# added: batched filter-spectrum loads in FFT mid pass; batched gate/running-sum loads in merge-GEMM epilogues (loads hoisted into dead fragment registers, one wait per batch)
# speedup vs baseline: 1.0340x; 1.0340x over previous
.LBB0_634:
	s_or_b64 exec, exec, s[0:1]
	v_readlane_b32 s0, v251, 28
	v_mov_b32_e32 v90, v173
	v_mov_b32_e32 v22, v178
	v_mov_b32_e32 v2, s0
	v_readlane_b32 s0, v251, 34
	v_mov_b32_e32 v23, v179
	v_mov_b32_e32 v10, v1
	s_waitcnt lgkmcnt(0)
	v_mov_b32_e32 v3, s0
	s_barrier
	ds_read_b128 v[6:9], v2
	ds_read_b128 v[2:5], v3
	v_mov_b32_e32 v60, v164
	v_mov_b32_e32 v34, v165
	v_mov_b32_e32 v62, v166
	v_mov_b32_e32 v32, v167
	v_mov_b32_e32 v64, v168
	v_mov_b32_e32 v38, v169
	v_mov_b32_e32 v66, v170
	v_mov_b32_e32 v10, v171
	v_pk_add_f32 v[68:69], v[14:15], v[42:43]
	v_pk_add_f32 v[14:15], v[14:15], v[42:43] neg_lo:[0,1] neg_hi:[0,1]
	s_nop 0
	v_mov_b32_e32 v13, v15
	v_mov_b32_e32 v10, v14
	v_mov_b32_e32 v42, v15
	v_mov_b32_e32 v43, v11
	v_pk_mul_f32 v[14:15], v[12:13], v[66:67] op_sel_hi:[1,0] neg_lo:[0,1] neg_hi:[0,1]
	v_pk_add_f32 v[70:71], v[18:19], v[52:53]
	v_pk_fma_f32 v[42:43], v[42:43], v[60:61], v[14:15] op_sel_hi:[1,0,1]
	v_pk_add_f32 v[14:15], v[16:17], v[48:49]
	v_pk_add_f32 v[48:49], v[16:17], v[48:49] neg_lo:[0,1] neg_hi:[0,1]
	v_mov_b32_e32 v17, v11
	v_mov_b32_e32 v13, v48
	v_mov_b32_e32 v16, v48
	v_pk_mul_f32 v[54:55], v[12:13], v[38:39] op_sel_hi:[1,0] neg_lo:[0,1] neg_hi:[0,1]
	v_mov_b32_e32 v13, v49
	v_pk_add_f32 v[18:19], v[18:19], v[52:53] neg_lo:[0,1] neg_hi:[0,1]
	v_pk_fma_f32 v[16:17], v[16:17], v[34:35], v[54:55] op_sel_hi:[1,0,1]
	v_mov_b32_e32 v54, v49
	v_mov_b32_e32 v55, v11
	v_pk_mul_f32 v[48:49], v[12:13], v[64:65] op_sel_hi:[1,0] neg_lo:[0,1] neg_hi:[0,1]
	v_mov_b32_e32 v13, v18
	v_pk_fma_f32 v[48:49], v[54:55], v[62:63], v[48:49] op_sel_hi:[1,0,1]
	v_mov_b32_e32 v52, v18
	v_mov_b32_e32 v53, v11
	v_pk_mul_f32 v[54:55], v[12:13], v[32:33] op_sel_hi:[1,0] neg_lo:[0,1] neg_hi:[0,1]
	v_mov_b32_e32 v13, v19
	v_pk_fma_f32 v[52:53], v[52:53], v[32:33], v[54:55] op_sel_hi:[1,0,1]
	v_mov_b32_e32 v54, v19
	v_mov_b32_e32 v55, v11
	v_pk_add_f32 v[18:19], v[20:21], v[50:51]
	v_pk_add_f32 v[20:21], v[20:21], v[50:51] neg_lo:[0,1] neg_hi:[0,1]
	v_pk_mul_f32 v[54:55], v[54:55], v[64:65] op_sel_hi:[1,0]
	v_mov_b32_e32 v50, v20
	v_mov_b32_e32 v51, v11
	v_pk_fma_f32 v[54:55], v[12:13], v[62:63], v[54:55] op_sel_hi:[1,0,1] neg_lo:[0,1,0] neg_hi:[0,1,0]
	v_pk_mul_f32 v[50:51], v[50:51], v[38:39] op_sel_hi:[1,0]
	v_mov_b32_e32 v13, v20
	v_pk_fma_f32 v[58:59], v[12:13], v[34:35], v[50:51] op_sel_hi:[1,0,1] neg_lo:[0,1,0] neg_hi:[0,1,0]
	v_mov_b32_e32 v50, v21
	v_mov_b32_e32 v51, v11
	v_pk_mul_f32 v[50:51], v[50:51], v[66:67] op_sel_hi:[1,0]
	v_mov_b32_e32 v13, v21
	v_pk_add_f32 v[20:21], v[26:27], v[46:47]
	v_pk_add_f32 v[26:27], v[26:27], v[46:47] neg_lo:[0,1] neg_hi:[0,1]
	v_pk_fma_f32 v[56:57], v[12:13], v[60:61], v[50:51] op_sel_hi:[1,0,1] neg_lo:[0,1,0] neg_hi:[0,1,0]
	v_xor_b32_e32 v73, 0x80000000, v26
	v_mov_b32_e32 v46, v27
	v_mov_b32_e32 v47, v11
	v_mov_b32_e32 v13, v27
	v_pk_add_f32 v[26:27], v[30:31], v[44:45]
	v_pk_add_f32 v[30:31], v[30:31], v[44:45] neg_lo:[0,1] neg_hi:[0,1]
	v_pk_mul_f32 v[46:47], v[46:47], v[66:67] op_sel_hi:[1,0] neg_lo:[0,1] neg_hi:[0,1]
	v_mov_b32_e32 v44, v30
	v_mov_b32_e32 v45, v11
	v_pk_fma_f32 v[74:75], v[12:13], v[60:61], v[46:47] op_sel_hi:[1,0,1] neg_lo:[0,1,0] neg_hi:[0,1,0]
	v_pk_mul_f32 v[44:45], v[44:45], v[38:39] op_sel_hi:[1,0] neg_lo:[0,1] neg_hi:[0,1]
	v_mov_b32_e32 v13, v30
	v_pk_fma_f32 v[76:77], v[12:13], v[34:35], v[44:45] op_sel_hi:[1,0,1] neg_lo:[0,1,0] neg_hi:[0,1,0]
	v_mov_b32_e32 v44, v31
	v_mov_b32_e32 v45, v11
	v_pk_mul_f32 v[44:45], v[44:45], v[64:65] op_sel_hi:[1,0] neg_lo:[0,1] neg_hi:[0,1]
	v_mov_b32_e32 v13, v31
	v_pk_add_f32 v[30:31], v[28:29], v[40:41]
	v_pk_add_f32 v[28:29], v[28:29], v[40:41] neg_lo:[0,1] neg_hi:[0,1]
	v_pk_fma_f32 v[78:79], v[12:13], v[62:63], v[44:45] op_sel_hi:[1,0,1] neg_lo:[0,1,0] neg_hi:[0,1,0]
	v_mov_b32_e32 v13, v28
	v_mov_b32_e32 v40, v28
	v_mov_b32_e32 v41, v11
	v_pk_mul_f32 v[44:45], v[12:13], v[32:33] op_sel_hi:[1,0] neg_lo:[0,1] neg_hi:[0,1]
	v_mov_b32_e32 v13, v29
	v_pk_fma_f32 v[80:81], v[40:41], v[32:33], v[44:45] op_sel_hi:[1,0,1] neg_lo:[0,1,0] neg_hi:[0,1,0]
	v_mov_b32_e32 v40, v29
	v_pk_mul_f32 v[28:29], v[12:13], v[64:65] op_sel_hi:[1,0] neg_lo:[0,1] neg_hi:[0,1]
	v_mov_b32_e32 v45, v11
	v_pk_fma_f32 v[62:63], v[40:41], v[62:63], v[28:29] op_sel_hi:[1,0,1] neg_lo:[0,1,0] neg_hi:[0,1,0]
	v_pk_add_f32 v[28:29], v[24:25], v[36:37]
	v_pk_add_f32 v[24:25], v[24:25], v[36:37] neg_lo:[0,1] neg_hi:[0,1]
	v_mov_b32_e32 v37, v11
	v_mov_b32_e32 v13, v24
	v_mov_b32_e32 v36, v24
	v_pk_mul_f32 v[40:41], v[12:13], v[38:39] op_sel_hi:[1,0] neg_lo:[0,1] neg_hi:[0,1]
	v_mov_b32_e32 v13, v25
	v_pk_fma_f32 v[64:65], v[36:37], v[34:35], v[40:41] op_sel_hi:[1,0,1] neg_lo:[0,1,0] neg_hi:[0,1,0]
	v_mov_b32_e32 v36, v25
	v_pk_mul_f32 v[24:25], v[12:13], v[66:67] op_sel_hi:[1,0] neg_lo:[0,1] neg_hi:[0,1]
	v_mov_b32_e32 v41, v11
	v_pk_fma_f32 v[66:67], v[36:37], v[60:61], v[24:25] op_sel_hi:[1,0,1] neg_lo:[0,1,0] neg_hi:[0,1,0]
	v_pk_add_f32 v[24:25], v[68:69], v[20:21] neg_lo:[0,1] neg_hi:[0,1]
	v_pk_add_f32 v[20:21], v[68:69], v[20:21]
	v_mov_b32_e32 v13, v25
	v_mov_b32_e32 v36, v24
	v_mov_b32_e32 v40, v25
	v_pk_mul_f32 v[24:25], v[12:13], v[38:39] op_sel_hi:[1,0] neg_lo:[0,1] neg_hi:[0,1]
	v_mov_b32_e32 v69, v11
	v_pk_fma_f32 v[24:25], v[40:41], v[34:35], v[24:25] op_sel_hi:[1,0,1]
	v_pk_add_f32 v[40:41], v[14:15], v[26:27] neg_lo:[0,1] neg_hi:[0,1]
	v_pk_add_f32 v[14:15], v[14:15], v[26:27]
	v_mov_b32_e32 v13, v40
	v_mov_b32_e32 v44, v40
	v_pk_mul_f32 v[46:47], v[12:13], v[32:33] op_sel_hi:[1,0] neg_lo:[0,1] neg_hi:[0,1]
	v_mov_b32_e32 v13, v41
	v_pk_fma_f32 v[44:45], v[44:45], v[32:33], v[46:47] op_sel_hi:[1,0,1]
	v_mov_b32_e32 v46, v41
	v_mov_b32_e32 v47, v11
	v_pk_mul_f32 v[46:47], v[46:47], v[38:39] op_sel_hi:[1,0]
	v_pk_add_f32 v[40:41], v[70:71], v[30:31] neg_lo:[0,1] neg_hi:[0,1]
	v_pk_fma_f32 v[50:51], v[12:13], v[34:35], v[46:47] op_sel_hi:[1,0,1] neg_lo:[0,1,0] neg_hi:[0,1,0]
	v_mov_b32_e32 v46, v41
	v_mov_b32_e32 v47, v11
	v_xor_b32_e32 v83, 0x80000000, v40
	v_pk_mul_f32 v[46:47], v[46:47], v[38:39] op_sel_hi:[1,0] neg_lo:[0,1] neg_hi:[0,1]
	v_mov_b32_e32 v13, v41
	v_pk_add_f32 v[40:41], v[18:19], v[28:29] neg_lo:[0,1] neg_hi:[0,1]
	v_pk_fma_f32 v[84:85], v[12:13], v[34:35], v[46:47] op_sel_hi:[1,0,1] neg_lo:[0,1,0] neg_hi:[0,1,0]
	v_mov_b32_e32 v13, v40
	v_pk_add_f32 v[26:27], v[70:71], v[30:31]
	v_mov_b32_e32 v46, v40
	v_mov_b32_e32 v47, v11
	v_pk_mul_f32 v[60:61], v[12:13], v[32:33] op_sel_hi:[1,0] neg_lo:[0,1] neg_hi:[0,1]
	v_mov_b32_e32 v13, v41
	v_pk_add_f32 v[18:19], v[18:19], v[28:29]
	v_pk_add_f32 v[28:29], v[20:21], v[26:27] neg_lo:[0,1] neg_hi:[0,1]
	v_pk_fma_f32 v[86:87], v[46:47], v[32:33], v[60:61] op_sel_hi:[1,0,1] neg_lo:[0,1,0] neg_hi:[0,1,0]
	v_mov_b32_e32 v46, v41
	v_pk_mul_f32 v[40:41], v[12:13], v[38:39] op_sel_hi:[1,0] neg_lo:[0,1] neg_hi:[0,1]
	v_mov_b32_e32 v13, v29
	v_pk_fma_f32 v[88:89], v[46:47], v[34:35], v[40:41] op_sel_hi:[1,0,1] neg_lo:[0,1,0] neg_hi:[0,1,0]
	v_mov_b32_e32 v40, v28
	v_pk_add_f32 v[20:21], v[20:21], v[26:27]
	v_mov_b32_e32 v26, v29
	v_mov_b32_e32 v27, v11
	v_pk_mul_f32 v[28:29], v[12:13], v[32:33] op_sel_hi:[1,0] neg_lo:[0,1] neg_hi:[0,1]
	v_mov_b32_e32 v41, v11
	v_pk_fma_f32 v[26:27], v[26:27], v[32:33], v[28:29] op_sel_hi:[1,0,1]
	v_pk_add_f32 v[28:29], v[14:15], v[18:19] neg_lo:[0,1] neg_hi:[0,1]
	v_pk_add_f32 v[14:15], v[14:15], v[18:19]
	v_mov_b32_e32 v13, v29
	v_xor_b32_e32 v61, 0x80000000, v28
	v_mov_b32_e32 v18, v29
	v_mov_b32_e32 v19, v11
	v_pk_mul_f32 v[28:29], v[12:13], v[32:33] op_sel_hi:[1,0] neg_lo:[0,1] neg_hi:[0,1]
	v_pk_add_f32 v[30:31], v[20:21], v[14:15]
	v_pk_fma_f32 v[18:19], v[18:19], v[32:33], v[28:29] op_sel_hi:[1,0,1] neg_lo:[0,1,0] neg_hi:[0,1,0]
	v_pk_add_f32 v[28:29], v[20:21], v[14:15] neg_lo:[0,1] neg_hi:[0,1]
	v_mov_b32_e32 v60, v11
	v_pk_add_f32 v[14:15], v[28:29], 0 neg_lo:[1,1] neg_hi:[1,1]
	v_mov_b32_e32 v68, v28
	v_mov_b32_e32 v14, v11
	v_pk_add_f32 v[46:47], v[68:69], v[14:15]
	v_pk_add_f32 v[20:21], v[68:69], v[14:15] neg_lo:[0,1] neg_hi:[0,1]
	v_pk_add_f32 v[14:15], v[40:41], v[60:61]
	v_pk_add_f32 v[28:29], v[40:41], v[60:61] neg_lo:[0,1] neg_hi:[0,1]
	v_pk_add_f32 v[40:41], v[26:27], v[18:19]
	v_pk_add_f32 v[18:19], v[26:27], v[18:19] neg_lo:[0,1] neg_hi:[0,1]
	v_mov_b32_e32 v82, v11
	v_xor_b32_e32 v69, 0x80000000, v18
	v_mov_b32_e32 v68, v19
	v_pk_add_f32 v[60:61], v[14:15], v[40:41]
	v_pk_add_f32 v[26:27], v[14:15], v[40:41] neg_lo:[0,1] neg_hi:[0,1]
	v_pk_add_f32 v[40:41], v[28:29], v[68:69]
	v_pk_add_f32 v[14:15], v[28:29], v[68:69] neg_lo:[0,1] neg_hi:[0,1]
	v_pk_add_f32 v[18:19], v[36:37], v[82:83]
	v_pk_add_f32 v[28:29], v[36:37], v[82:83] neg_lo:[0,1] neg_hi:[0,1]
	v_pk_add_f32 v[36:37], v[24:25], v[84:85]
	v_pk_add_f32 v[24:25], v[24:25], v[84:85] neg_lo:[0,1] neg_hi:[0,1]
	v_mov_b32_e32 v72, v11
	v_xor_b32_e32 v68, 0x80000000, v25
	v_mov_b32_e32 v69, v24
	v_pk_mul_f32 v[68:69], v[32:33], v[68:69] op_sel_hi:[0,1] neg_lo:[1,0] neg_hi:[1,0]
	v_pk_fma_f32 v[68:69], v[32:33], v[24:25], v[68:69] op_sel_hi:[0,1,1]
	v_pk_add_f32 v[24:25], v[44:45], v[86:87]
	v_pk_add_f32 v[44:45], v[44:45], v[86:87] neg_lo:[0,1] neg_hi:[0,1]
	v_lshl_add_u32 v13, v90, 3, 0
	v_xor_b32_e32 v71, 0x80000000, v44
	v_mov_b32_e32 v70, v45
	v_pk_add_f32 v[44:45], v[50:51], v[88:89]
	v_pk_add_f32 v[50:51], v[50:51], v[88:89] neg_lo:[0,1] neg_hi:[0,1]
	s_nop 0
	v_xor_b32_e32 v82, 0x80000000, v51
	v_mov_b32_e32 v83, v50
	v_pk_mul_f32 v[82:83], v[32:33], v[82:83] op_sel_hi:[0,1] neg_lo:[1,0] neg_hi:[1,0]
	v_pk_fma_f32 v[82:83], v[32:33], v[50:51], v[82:83] op_sel_hi:[0,1,1] neg_lo:[1,0,0] neg_hi:[1,0,0]
	v_pk_add_f32 v[50:51], v[18:19], v[24:25]
	v_pk_add_f32 v[18:19], v[18:19], v[24:25] neg_lo:[0,1] neg_hi:[0,1]
	v_pk_add_f32 v[24:25], v[36:37], v[44:45]
	v_pk_add_f32 v[36:37], v[36:37], v[44:45] neg_lo:[0,1] neg_hi:[0,1]
	v_pk_add_f32 v[84:85], v[50:51], v[24:25]
	v_xor_b32_e32 v45, 0x80000000, v36
	v_mov_b32_e32 v44, v37
	v_pk_add_f32 v[36:37], v[50:51], v[24:25] neg_lo:[0,1] neg_hi:[0,1]
	v_pk_add_f32 v[50:51], v[18:19], v[44:45]
	v_pk_add_f32 v[24:25], v[18:19], v[44:45] neg_lo:[0,1] neg_hi:[0,1]
	v_pk_add_f32 v[44:45], v[68:69], v[82:83] neg_lo:[0,1] neg_hi:[0,1]
	v_pk_add_f32 v[18:19], v[28:29], v[70:71]
	v_pk_add_f32 v[70:71], v[28:29], v[70:71] neg_lo:[0,1] neg_hi:[0,1]
	v_pk_add_f32 v[28:29], v[68:69], v[82:83]
	v_xor_b32_e32 v69, 0x80000000, v44
	v_mov_b32_e32 v68, v45
	v_pk_add_f32 v[82:83], v[18:19], v[28:29]
	v_pk_add_f32 v[28:29], v[18:19], v[28:29] neg_lo:[0,1] neg_hi:[0,1]
	v_pk_add_f32 v[44:45], v[70:71], v[68:69]
	v_pk_add_f32 v[18:19], v[70:71], v[68:69] neg_lo:[0,1] neg_hi:[0,1]
	v_pk_add_f32 v[68:69], v[10:11], v[72:73]
	v_pk_add_f32 v[70:71], v[10:11], v[72:73] neg_lo:[0,1] neg_hi:[0,1]
	v_pk_add_f32 v[72:73], v[42:43], v[74:75]
	v_pk_add_f32 v[42:43], v[42:43], v[74:75] neg_lo:[0,1] neg_hi:[0,1]
	v_add_f32_e32 v10, v30, v31
	v_xor_b32_e32 v74, 0x80000000, v43
	v_mov_b32_e32 v75, v42
	v_pk_mul_f32 v[74:75], v[38:39], v[74:75] op_sel_hi:[0,1] neg_lo:[1,0] neg_hi:[1,0]
	v_pk_fma_f32 v[42:43], v[34:35], v[42:43], v[74:75] op_sel_hi:[0,1,1]
	v_pk_add_f32 v[74:75], v[16:17], v[76:77]
	v_pk_add_f32 v[16:17], v[16:17], v[76:77] neg_lo:[0,1] neg_hi:[0,1]
	s_nop 0
	v_xor_b32_e32 v76, 0x80000000, v17
	v_mov_b32_e32 v77, v16
	v_pk_mul_f32 v[76:77], v[32:33], v[76:77] op_sel_hi:[0,1] neg_lo:[1,0] neg_hi:[1,0]
	v_pk_fma_f32 v[16:17], v[32:33], v[16:17], v[76:77] op_sel_hi:[0,1,1]
	v_pk_add_f32 v[76:77], v[48:49], v[78:79]
	v_pk_add_f32 v[48:49], v[48:49], v[78:79] neg_lo:[0,1] neg_hi:[0,1]
	s_nop 0
	v_xor_b32_e32 v78, 0x80000000, v49
	v_mov_b32_e32 v79, v48
	v_pk_mul_f32 v[78:79], v[34:35], v[78:79] op_sel_hi:[0,1] neg_lo:[1,0] neg_hi:[1,0]
	v_pk_fma_f32 v[78:79], v[38:39], v[48:49], v[78:79] op_sel_hi:[0,1,1]
	v_pk_add_f32 v[48:49], v[52:53], v[80:81]
	v_pk_add_f32 v[52:53], v[52:53], v[80:81] neg_lo:[0,1] neg_hi:[0,1]
	s_nop 0
	v_xor_b32_e32 v81, 0x80000000, v52
	v_mov_b32_e32 v80, v53
	v_pk_add_f32 v[52:53], v[54:55], v[62:63]
	v_pk_add_f32 v[54:55], v[54:55], v[62:63] neg_lo:[0,1] neg_hi:[0,1]
	s_nop 0
	v_xor_b32_e32 v62, 0x80000000, v55
	v_mov_b32_e32 v63, v54
	v_pk_mul_f32 v[62:63], v[34:35], v[62:63] op_sel_hi:[0,1] neg_lo:[1,0] neg_hi:[1,0]
	v_pk_fma_f32 v[62:63], v[38:39], v[54:55], v[62:63] op_sel_hi:[0,1,1] neg_lo:[1,0,0] neg_hi:[1,0,0]
	v_pk_add_f32 v[54:55], v[58:59], v[64:65]
	v_pk_add_f32 v[58:59], v[58:59], v[64:65] neg_lo:[0,1] neg_hi:[0,1]
	s_nop 0
	v_xor_b32_e32 v64, 0x80000000, v59
	v_mov_b32_e32 v65, v58
	v_pk_mul_f32 v[64:65], v[32:33], v[64:65] op_sel_hi:[0,1] neg_lo:[1,0] neg_hi:[1,0]
	v_pk_fma_f32 v[58:59], v[32:33], v[58:59], v[64:65] op_sel_hi:[0,1,1] neg_lo:[1,0,0] neg_hi:[1,0,0]
	v_pk_add_f32 v[64:65], v[56:57], v[66:67]
	v_pk_add_f32 v[56:57], v[56:57], v[66:67] neg_lo:[0,1] neg_hi:[0,1]
	s_nop 0
	v_xor_b32_e32 v66, 0x80000000, v57
	v_mov_b32_e32 v67, v56
	v_pk_mul_f32 v[38:39], v[38:39], v[66:67] op_sel_hi:[0,1] neg_lo:[1,0] neg_hi:[1,0]
	v_pk_fma_f32 v[56:57], v[34:35], v[56:57], v[38:39] op_sel_hi:[0,1,1] neg_lo:[1,0,0] neg_hi:[1,0,0]
	v_pk_add_f32 v[38:39], v[52:53], v[72:73]
	v_pk_add_f32 v[52:53], v[72:73], v[52:53] neg_lo:[0,1] neg_hi:[0,1]
	v_pk_add_f32 v[34:35], v[68:69], v[48:49]
	v_xor_b32_e32 v66, 0x80000000, v53
	v_mov_b32_e32 v67, v52
	v_pk_mul_f32 v[66:67], v[32:33], v[66:67] op_sel_hi:[0,1] neg_lo:[1,0] neg_hi:[1,0]
	v_pk_fma_f32 v[52:53], v[32:33], v[52:53], v[66:67] op_sel_hi:[0,1,1]
	v_pk_add_f32 v[66:67], v[74:75], v[54:55]
	v_pk_add_f32 v[54:55], v[74:75], v[54:55] neg_lo:[0,1] neg_hi:[0,1]
	v_pk_add_f32 v[48:49], v[68:69], v[48:49] neg_lo:[0,1] neg_hi:[0,1]
	v_xor_b32_e32 v69, 0x80000000, v54
	v_mov_b32_e32 v68, v55
	v_pk_add_f32 v[54:55], v[76:77], v[64:65]
	v_pk_add_f32 v[64:65], v[76:77], v[64:65] neg_lo:[0,1] neg_hi:[0,1]
	s_nop 0
	v_xor_b32_e32 v72, 0x80000000, v65
	v_mov_b32_e32 v73, v64
	v_pk_mul_f32 v[72:73], v[32:33], v[72:73] op_sel_hi:[0,1] neg_lo:[1,0] neg_hi:[1,0]
	v_pk_fma_f32 v[64:65], v[32:33], v[64:65], v[72:73] op_sel_hi:[0,1,1] neg_lo:[1,0,0] neg_hi:[1,0,0]
	v_pk_add_f32 v[72:73], v[34:35], v[66:67]
	v_pk_add_f32 v[34:35], v[34:35], v[66:67] neg_lo:[0,1] neg_hi:[0,1]
	v_pk_add_f32 v[66:67], v[38:39], v[54:55]
	v_pk_add_f32 v[38:39], v[38:39], v[54:55] neg_lo:[0,1] neg_hi:[0,1]
	v_pk_add_f32 v[76:77], v[72:73], v[66:67]
	v_xor_b32_e32 v75, 0x80000000, v38
	v_mov_b32_e32 v74, v39
	v_pk_add_f32 v[54:55], v[72:73], v[66:67] neg_lo:[0,1] neg_hi:[0,1]
	v_pk_add_f32 v[66:67], v[34:35], v[74:75]
	v_pk_add_f32 v[38:39], v[34:35], v[74:75] neg_lo:[0,1] neg_hi:[0,1]
	v_pk_add_f32 v[34:35], v[48:49], v[68:69]
	v_pk_add_f32 v[68:69], v[48:49], v[68:69] neg_lo:[0,1] neg_hi:[0,1]
	v_pk_add_f32 v[48:49], v[52:53], v[64:65]
	v_pk_add_f32 v[52:53], v[52:53], v[64:65] neg_lo:[0,1] neg_hi:[0,1]
	v_pk_add_f32 v[72:73], v[34:35], v[48:49]
	v_xor_b32_e32 v65, 0x80000000, v52
	v_mov_b32_e32 v64, v53
	v_pk_add_f32 v[48:49], v[34:35], v[48:49] neg_lo:[0,1] neg_hi:[0,1]
	v_pk_add_f32 v[74:75], v[68:69], v[64:65]
	v_pk_add_f32 v[34:35], v[68:69], v[64:65] neg_lo:[0,1] neg_hi:[0,1]
	v_pk_add_f32 v[68:69], v[62:63], v[42:43]
	v_pk_add_f32 v[42:43], v[42:43], v[62:63] neg_lo:[0,1] neg_hi:[0,1]
	v_pk_add_f32 v[52:53], v[70:71], v[80:81]
	v_xor_b32_e32 v62, 0x80000000, v43
	v_mov_b32_e32 v63, v42
	v_pk_mul_f32 v[62:63], v[32:33], v[62:63] op_sel_hi:[0,1] neg_lo:[1,0] neg_hi:[1,0]
	v_pk_fma_f32 v[62:63], v[32:33], v[42:43], v[62:63] op_sel_hi:[0,1,1]
	v_pk_add_f32 v[42:43], v[16:17], v[58:59]
	v_pk_add_f32 v[16:17], v[16:17], v[58:59] neg_lo:[0,1] neg_hi:[0,1]
	v_pk_add_f32 v[64:65], v[70:71], v[80:81] neg_lo:[0,1] neg_hi:[0,1]
	v_xor_b32_e32 v59, 0x80000000, v16
	v_mov_b32_e32 v58, v17
	v_pk_add_f32 v[16:17], v[78:79], v[56:57]
	v_pk_add_f32 v[56:57], v[78:79], v[56:57] neg_lo:[0,1] neg_hi:[0,1]
	s_nop 0
	v_xor_b32_e32 v70, 0x80000000, v57
	v_mov_b32_e32 v71, v56
	v_pk_mul_f32 v[70:71], v[32:33], v[70:71] op_sel_hi:[0,1] neg_lo:[1,0] neg_hi:[1,0]
	v_pk_fma_f32 v[32:33], v[32:33], v[56:57], v[70:71] op_sel_hi:[0,1,1] neg_lo:[1,0,0] neg_hi:[1,0,0]
	v_pk_add_f32 v[56:57], v[52:53], v[42:43]
	v_pk_add_f32 v[42:43], v[52:53], v[42:43] neg_lo:[0,1] neg_hi:[0,1]
	v_pk_add_f32 v[52:53], v[68:69], v[16:17]
	v_pk_add_f32 v[16:17], v[68:69], v[16:17] neg_lo:[0,1] neg_hi:[0,1]
	v_pk_add_f32 v[70:71], v[56:57], v[52:53]
	v_xor_b32_e32 v69, 0x80000000, v16
	v_mov_b32_e32 v68, v17
	v_pk_add_f32 v[56:57], v[56:57], v[52:53] neg_lo:[0,1] neg_hi:[0,1]
	v_pk_add_f32 v[16:17], v[64:65], v[58:59]
	v_pk_add_f32 v[52:53], v[62:63], v[32:33]
	v_pk_add_f32 v[32:33], v[62:63], v[32:33] neg_lo:[0,1] neg_hi:[0,1]
	v_pk_add_f32 v[58:59], v[64:65], v[58:59] neg_lo:[0,1] neg_hi:[0,1]
	v_xor_b32_e32 v63, 0x80000000, v32
	v_mov_b32_e32 v62, v33
	v_pk_add_f32 v[64:65], v[16:17], v[52:53]
	v_pk_add_f32 v[52:53], v[16:17], v[52:53] neg_lo:[0,1] neg_hi:[0,1]
	v_mov_b64_e32 v[16:17], s[90:91]
	v_pk_add_f32 v[78:79], v[42:43], v[68:69]
	v_pk_add_f32 v[42:43], v[42:43], v[68:69] neg_lo:[0,1] neg_hi:[0,1]
	v_pk_add_f32 v[68:69], v[58:59], v[62:63]
	v_pk_add_f32 v[32:33], v[58:59], v[62:63] neg_lo:[0,1] neg_hi:[0,1]
	v_pk_fma_f32 v[58:59], v[10:11], s[94:95], v[16:17] op_sel_hi:[0,1,1]
	ds_write_b64 v13, v[58:59]
	v_pk_fma_f32 v[58:59], v[22:23], s[90:91], v[22:23] op_sel:[1,0,0] op_sel_hi:[0,1,1]
	v_xor_b32_e32 v62, 0x80000000, v77
	v_mov_b32_e32 v63, v77
	v_pk_mul_f32 v[62:63], v[58:59], v[62:63] op_sel:[1,0] op_sel_hi:[0,1]
	v_pk_fma_f32 v[62:63], v[58:59], v[76:77], v[62:63] op_sel_hi:[1,0,1]
	ds_write_b64 v13, v[62:63] offset:4224
	v_xor_b32_e32 v62, 0x80000000, v59
	v_mov_b32_e32 v63, v59
	v_pk_mul_f32 v[62:63], v[22:23], v[62:63] op_sel:[1,0] op_sel_hi:[0,1]
	v_pk_fma_f32 v[58:59], v[22:23], v[58:59], v[62:63] op_sel_hi:[1,0,1]
	v_xor_b32_e32 v62, 0x80000000, v85
	v_mov_b32_e32 v63, v85
	v_pk_mul_f32 v[62:63], v[58:59], v[62:63] op_sel:[1,0] op_sel_hi:[0,1]
	v_pk_fma_f32 v[62:63], v[58:59], v[84:85], v[62:63] op_sel_hi:[1,0,1]
	ds_write_b64 v13, v[62:63] offset:8448
	v_xor_b32_e32 v62, 0x80000000, v59
	v_mov_b32_e32 v63, v59
	v_pk_mul_f32 v[62:63], v[22:23], v[62:63] op_sel:[1,0] op_sel_hi:[0,1]
	v_pk_fma_f32 v[58:59], v[22:23], v[58:59], v[62:63] op_sel_hi:[1,0,1]
	v_xor_b32_e32 v62, 0x80000000, v71
	v_mov_b32_e32 v63, v71
	v_pk_mul_f32 v[62:63], v[58:59], v[62:63] op_sel:[1,0] op_sel_hi:[0,1]
	v_pk_fma_f32 v[62:63], v[58:59], v[70:71], v[62:63] op_sel_hi:[1,0,1]
	ds_write_b64 v13, v[62:63] offset:12672
	v_xor_b32_e32 v62, 0x80000000, v59
	v_mov_b32_e32 v63, v59
	v_pk_mul_f32 v[62:63], v[22:23], v[62:63] op_sel:[1,0] op_sel_hi:[0,1]
	v_pk_fma_f32 v[58:59], v[22:23], v[58:59], v[62:63] op_sel_hi:[1,0,1]
	v_xor_b32_e32 v62, 0x80000000, v61
	v_mov_b32_e32 v63, v61
	v_pk_mul_f32 v[62:63], v[62:63], v[58:59] op_sel:[0,1] op_sel_hi:[1,0]
	s_nop 0
	v_pk_fma_f32 v[60:61], v[60:61], v[58:59], v[62:63] op_sel_hi:[0,1,1]
	ds_write_b64 v13, v[60:61] offset:16896
	v_xor_b32_e32 v60, 0x80000000, v59
	v_mov_b32_e32 v61, v59
	v_pk_mul_f32 v[60:61], v[22:23], v[60:61] op_sel:[1,0] op_sel_hi:[0,1]
	v_pk_fma_f32 v[58:59], v[22:23], v[58:59], v[60:61] op_sel_hi:[1,0,1]
	v_xor_b32_e32 v60, 0x80000000, v73
	v_mov_b32_e32 v61, v73
	v_pk_mul_f32 v[60:61], v[58:59], v[60:61] op_sel:[1,0] op_sel_hi:[0,1]
	v_pk_fma_f32 v[60:61], v[58:59], v[72:73], v[60:61] op_sel_hi:[1,0,1]
	ds_write_b64 v13, v[60:61] offset:21120
	v_xor_b32_e32 v60, 0x80000000, v59
	v_mov_b32_e32 v61, v59
	v_pk_mul_f32 v[60:61], v[22:23], v[60:61] op_sel:[1,0] op_sel_hi:[0,1]
	v_pk_fma_f32 v[58:59], v[22:23], v[58:59], v[60:61] op_sel_hi:[1,0,1]
	v_xor_b32_e32 v60, 0x80000000, v83
	v_mov_b32_e32 v61, v83
	v_pk_mul_f32 v[60:61], v[60:61], v[58:59] op_sel:[0,1] op_sel_hi:[1,0]
	s_nop 0
	v_pk_fma_f32 v[60:61], v[82:83], v[58:59], v[60:61] op_sel_hi:[0,1,1]
	ds_write_b64 v13, v[60:61] offset:25344
	v_xor_b32_e32 v60, 0x80000000, v59
	v_mov_b32_e32 v61, v59
	v_pk_mul_f32 v[60:61], v[22:23], v[60:61] op_sel:[1,0] op_sel_hi:[0,1]
	v_pk_fma_f32 v[58:59], v[22:23], v[58:59], v[60:61] op_sel_hi:[1,0,1]
	v_xor_b32_e32 v60, 0x80000000, v65
	v_mov_b32_e32 v61, v65
	v_pk_mul_f32 v[60:61], v[60:61], v[58:59] op_sel:[0,1] op_sel_hi:[1,0]
	s_nop 0
	v_pk_fma_f32 v[60:61], v[64:65], v[58:59], v[60:61] op_sel_hi:[0,1,1]
	ds_write_b64 v13, v[60:61] offset:29568
	v_xor_b32_e32 v60, 0x80000000, v59
	v_mov_b32_e32 v61, v59
	v_pk_mul_f32 v[60:61], v[22:23], v[60:61] op_sel:[1,0] op_sel_hi:[0,1]
	v_pk_fma_f32 v[58:59], v[22:23], v[58:59], v[60:61] op_sel_hi:[1,0,1]
	v_xor_b32_e32 v60, 0x80000000, v47
	v_mov_b32_e32 v61, v47
	v_pk_mul_f32 v[60:61], v[60:61], v[58:59] op_sel:[0,1] op_sel_hi:[1,0]
	s_nop 0
	v_pk_fma_f32 v[46:47], v[46:47], v[58:59], v[60:61] op_sel_hi:[0,1,1]
	ds_write_b64 v13, v[46:47] offset:33792
	v_xor_b32_e32 v46, 0x80000000, v59
	v_mov_b32_e32 v47, v59
	v_pk_mul_f32 v[46:47], v[22:23], v[46:47] op_sel:[1,0] op_sel_hi:[0,1]
	v_pk_fma_f32 v[46:47], v[22:23], v[58:59], v[46:47] op_sel_hi:[1,0,1]
	v_xor_b32_e32 v58, 0x80000000, v67
	v_mov_b32_e32 v59, v67
	v_pk_mul_f32 v[58:59], v[58:59], v[46:47] op_sel:[0,1] op_sel_hi:[1,0]
	s_nop 0
	v_pk_fma_f32 v[58:59], v[66:67], v[46:47], v[58:59] op_sel_hi:[0,1,1]
	ds_write_b64 v13, v[58:59] offset:38016
	v_xor_b32_e32 v58, 0x80000000, v47
	v_mov_b32_e32 v59, v47
	v_pk_mul_f32 v[58:59], v[22:23], v[58:59] op_sel:[1,0] op_sel_hi:[0,1]
	v_pk_fma_f32 v[46:47], v[22:23], v[46:47], v[58:59] op_sel_hi:[1,0,1]
	v_xor_b32_e32 v58, 0x80000000, v51
	v_mov_b32_e32 v59, v51
	v_pk_mul_f32 v[58:59], v[58:59], v[46:47] op_sel:[0,1] op_sel_hi:[1,0]
	s_nop 0
	v_pk_fma_f32 v[50:51], v[50:51], v[46:47], v[58:59] op_sel_hi:[0,1,1]
	ds_write_b64 v13, v[50:51] offset:42240
	v_xor_b32_e32 v50, 0x80000000, v47
	v_mov_b32_e32 v51, v47
	v_pk_mul_f32 v[50:51], v[22:23], v[50:51] op_sel:[1,0] op_sel_hi:[0,1]
	v_pk_fma_f32 v[46:47], v[22:23], v[46:47], v[50:51] op_sel_hi:[1,0,1]
	v_xor_b32_e32 v50, 0x80000000, v79
	v_mov_b32_e32 v51, v79
	v_pk_mul_f32 v[50:51], v[50:51], v[46:47] op_sel:[0,1] op_sel_hi:[1,0]
	s_nop 0
	v_pk_fma_f32 v[50:51], v[78:79], v[46:47], v[50:51] op_sel_hi:[0,1,1]
	ds_write_b64 v13, v[50:51] offset:46464
	v_xor_b32_e32 v50, 0x80000000, v47
	v_mov_b32_e32 v51, v47
	v_pk_mul_f32 v[50:51], v[22:23], v[50:51] op_sel:[1,0] op_sel_hi:[0,1]
	v_pk_fma_f32 v[46:47], v[22:23], v[46:47], v[50:51] op_sel_hi:[1,0,1]
	v_xor_b32_e32 v50, 0x80000000, v41
	v_mov_b32_e32 v51, v41
	v_pk_mul_f32 v[50:51], v[50:51], v[46:47] op_sel:[0,1] op_sel_hi:[1,0]
	s_nop 0
	v_pk_fma_f32 v[40:41], v[40:41], v[46:47], v[50:51] op_sel_hi:[0,1,1]
	ds_write_b64 v13, v[40:41] offset:50688
	v_xor_b32_e32 v40, 0x80000000, v47
	v_mov_b32_e32 v41, v47
	v_pk_mul_f32 v[40:41], v[22:23], v[40:41] op_sel:[1,0] op_sel_hi:[0,1]
	v_pk_fma_f32 v[40:41], v[22:23], v[46:47], v[40:41] op_sel_hi:[1,0,1]
	v_xor_b32_e32 v46, 0x80000000, v75
	v_mov_b32_e32 v47, v75
	v_pk_mul_f32 v[46:47], v[46:47], v[40:41] op_sel:[0,1] op_sel_hi:[1,0]
	s_nop 0
	v_pk_fma_f32 v[46:47], v[74:75], v[40:41], v[46:47] op_sel_hi:[0,1,1]
	ds_write_b64 v13, v[46:47] offset:54912
	v_xor_b32_e32 v46, 0x80000000, v41
	v_mov_b32_e32 v47, v41
	v_pk_mul_f32 v[46:47], v[22:23], v[46:47] op_sel:[1,0] op_sel_hi:[0,1]
	v_pk_fma_f32 v[40:41], v[22:23], v[40:41], v[46:47] op_sel_hi:[1,0,1]
	v_xor_b32_e32 v46, 0x80000000, v45
	v_mov_b32_e32 v47, v45
	v_pk_mul_f32 v[46:47], v[46:47], v[40:41] op_sel:[0,1] op_sel_hi:[1,0]
	s_nop 0
	v_pk_fma_f32 v[44:45], v[44:45], v[40:41], v[46:47] op_sel_hi:[0,1,1]
	ds_write_b64 v13, v[44:45] offset:59136
	v_xor_b32_e32 v44, 0x80000000, v41
	v_mov_b32_e32 v45, v41
	v_pk_mul_f32 v[44:45], v[22:23], v[44:45] op_sel:[1,0] op_sel_hi:[0,1]
	v_pk_fma_f32 v[40:41], v[22:23], v[40:41], v[44:45] op_sel_hi:[1,0,1]
	v_xor_b32_e32 v44, 0x80000000, v69
	v_mov_b32_e32 v45, v69
	v_pk_mul_f32 v[44:45], v[44:45], v[40:41] op_sel:[0,1] op_sel_hi:[1,0]
	s_nop 0
	v_pk_fma_f32 v[44:45], v[68:69], v[40:41], v[44:45] op_sel_hi:[0,1,1]
	ds_write_b64 v13, v[44:45] offset:63360
	v_xor_b32_e32 v44, 0x80000000, v41
	v_mov_b32_e32 v45, v41
	v_pk_mul_f32 v[44:45], v[22:23], v[44:45] op_sel:[1,0] op_sel_hi:[0,1]
	v_pk_fma_f32 v[40:41], v[22:23], v[40:41], v[44:45] op_sel_hi:[1,0,1]
	s_mov_b32 s44, s95
	v_sub_f32_e32 v10, v30, v31
	v_pk_mul_f32 v[30:31], v[40:41], s[44:45]
	s_nop 0
	v_pk_fma_f32 v[30:31], v[10:11], v[40:41], v[30:31] op_sel:[0,0,1] op_sel_hi:[0,1,0]
	v_add_u32_e32 v10, 0x10800, v13
	ds_write_b64 v10, v[30:31]
	v_xor_b32_e32 v30, 0x80000000, v41
	v_mov_b32_e32 v31, v41
	v_pk_mul_f32 v[30:31], v[22:23], v[30:31] op_sel:[1,0] op_sel_hi:[0,1]
	v_pk_fma_f32 v[30:31], v[22:23], v[40:41], v[30:31] op_sel_hi:[1,0,1]
	v_xor_b32_e32 v40, 0x80000000, v55
	v_mov_b32_e32 v41, v55
	v_pk_mul_f32 v[40:41], v[40:41], v[30:31] op_sel:[0,1] op_sel_hi:[1,0]
	v_add_u32_e32 v10, 0x11880, v13
	v_pk_fma_f32 v[40:41], v[54:55], v[30:31], v[40:41] op_sel_hi:[0,1,1]
	ds_write_b64 v10, v[40:41]
	v_xor_b32_e32 v40, 0x80000000, v31
	v_mov_b32_e32 v41, v31
	v_pk_mul_f32 v[40:41], v[22:23], v[40:41] op_sel:[1,0] op_sel_hi:[0,1]
	v_pk_fma_f32 v[30:31], v[22:23], v[30:31], v[40:41] op_sel_hi:[1,0,1]
	v_xor_b32_e32 v40, 0x80000000, v37
	v_mov_b32_e32 v41, v37
	v_pk_mul_f32 v[40:41], v[40:41], v[30:31] op_sel:[0,1] op_sel_hi:[1,0]
	v_add_u32_e32 v10, 0x12900, v13
	v_pk_fma_f32 v[36:37], v[36:37], v[30:31], v[40:41] op_sel_hi:[0,1,1]
	ds_write_b64 v10, v[36:37]
	v_xor_b32_e32 v36, 0x80000000, v31
	v_mov_b32_e32 v37, v31
	v_pk_mul_f32 v[36:37], v[22:23], v[36:37] op_sel:[1,0] op_sel_hi:[0,1]
	v_pk_fma_f32 v[30:31], v[22:23], v[30:31], v[36:37] op_sel_hi:[1,0,1]
	v_xor_b32_e32 v36, 0x80000000, v57
	v_mov_b32_e32 v37, v57
	v_pk_mul_f32 v[36:37], v[36:37], v[30:31] op_sel:[0,1] op_sel_hi:[1,0]
	v_add_u32_e32 v10, 0x13980, v13
	v_pk_fma_f32 v[36:37], v[56:57], v[30:31], v[36:37] op_sel_hi:[0,1,1]
	ds_write_b64 v10, v[36:37]
	v_xor_b32_e32 v36, 0x80000000, v31
	v_mov_b32_e32 v37, v31
	v_pk_mul_f32 v[36:37], v[22:23], v[36:37] op_sel:[1,0] op_sel_hi:[0,1]
	v_pk_fma_f32 v[30:31], v[22:23], v[30:31], v[36:37] op_sel_hi:[1,0,1]
	v_xor_b32_e32 v36, 0x80000000, v27
	v_mov_b32_e32 v37, v27
	v_pk_mul_f32 v[36:37], v[36:37], v[30:31] op_sel:[0,1] op_sel_hi:[1,0]
	v_add_u32_e32 v10, 0x14a00, v13
	v_pk_fma_f32 v[26:27], v[26:27], v[30:31], v[36:37] op_sel_hi:[0,1,1]
	ds_write_b64 v10, v[26:27]
	v_xor_b32_e32 v26, 0x80000000, v31
	v_mov_b32_e32 v27, v31
	v_pk_mul_f32 v[26:27], v[22:23], v[26:27] op_sel:[1,0] op_sel_hi:[0,1]
	v_pk_fma_f32 v[26:27], v[22:23], v[30:31], v[26:27] op_sel_hi:[1,0,1]
	v_xor_b32_e32 v30, 0x80000000, v49
	v_mov_b32_e32 v31, v49
	v_pk_mul_f32 v[30:31], v[30:31], v[26:27] op_sel:[0,1] op_sel_hi:[1,0]
	v_add_u32_e32 v10, 0x15a80, v13
	v_pk_fma_f32 v[30:31], v[48:49], v[26:27], v[30:31] op_sel_hi:[0,1,1]
	ds_write_b64 v10, v[30:31]
	v_xor_b32_e32 v30, 0x80000000, v27
	v_mov_b32_e32 v31, v27
	v_pk_mul_f32 v[30:31], v[22:23], v[30:31] op_sel:[1,0] op_sel_hi:[0,1]
	v_pk_fma_f32 v[26:27], v[22:23], v[26:27], v[30:31] op_sel_hi:[1,0,1]
	v_xor_b32_e32 v30, 0x80000000, v29
	v_mov_b32_e32 v31, v29
	v_pk_mul_f32 v[30:31], v[30:31], v[26:27] op_sel:[0,1] op_sel_hi:[1,0]
	v_add_u32_e32 v10, 0x16b00, v13
	v_pk_fma_f32 v[28:29], v[28:29], v[26:27], v[30:31] op_sel_hi:[0,1,1]
	ds_write_b64 v10, v[28:29]
	v_xor_b32_e32 v28, 0x80000000, v27
	v_mov_b32_e32 v29, v27
	v_pk_mul_f32 v[28:29], v[22:23], v[28:29] op_sel:[1,0] op_sel_hi:[0,1]
	v_pk_fma_f32 v[26:27], v[22:23], v[26:27], v[28:29] op_sel_hi:[1,0,1]
	v_xor_b32_e32 v28, 0x80000000, v53
	v_mov_b32_e32 v29, v53
	v_pk_mul_f32 v[28:29], v[28:29], v[26:27] op_sel:[0,1] op_sel_hi:[1,0]
	v_add_u32_e32 v10, 0x17b80, v13
	v_pk_fma_f32 v[28:29], v[52:53], v[26:27], v[28:29] op_sel_hi:[0,1,1]
	ds_write_b64 v10, v[28:29]
	v_xor_b32_e32 v28, 0x80000000, v27
	v_mov_b32_e32 v29, v27
	v_pk_mul_f32 v[28:29], v[22:23], v[28:29] op_sel:[1,0] op_sel_hi:[0,1]
	v_pk_fma_f32 v[26:27], v[22:23], v[26:27], v[28:29] op_sel_hi:[1,0,1]
	v_xor_b32_e32 v28, 0x80000000, v21
	v_mov_b32_e32 v29, v21
	v_pk_mul_f32 v[28:29], v[28:29], v[26:27] op_sel:[0,1] op_sel_hi:[1,0]
	v_add_u32_e32 v10, 0x18c00, v13
	v_pk_fma_f32 v[20:21], v[20:21], v[26:27], v[28:29] op_sel_hi:[0,1,1]
	ds_write_b64 v10, v[20:21]
	v_xor_b32_e32 v20, 0x80000000, v27
	v_mov_b32_e32 v21, v27
	v_pk_mul_f32 v[20:21], v[22:23], v[20:21] op_sel:[1,0] op_sel_hi:[0,1]
	v_pk_fma_f32 v[20:21], v[22:23], v[26:27], v[20:21] op_sel_hi:[1,0,1]
	v_xor_b32_e32 v26, 0x80000000, v39
	v_mov_b32_e32 v27, v39
	v_pk_mul_f32 v[26:27], v[26:27], v[20:21] op_sel:[0,1] op_sel_hi:[1,0]
	v_add_u32_e32 v10, 0x19c80, v13
	v_pk_fma_f32 v[26:27], v[38:39], v[20:21], v[26:27] op_sel_hi:[0,1,1]
	ds_write_b64 v10, v[26:27]
	v_xor_b32_e32 v26, 0x80000000, v21
	v_mov_b32_e32 v27, v21
	v_pk_mul_f32 v[26:27], v[22:23], v[26:27] op_sel:[1,0] op_sel_hi:[0,1]
	v_pk_fma_f32 v[20:21], v[22:23], v[20:21], v[26:27] op_sel_hi:[1,0,1]
	v_xor_b32_e32 v26, 0x80000000, v25
	v_mov_b32_e32 v27, v25
	v_pk_mul_f32 v[26:27], v[26:27], v[20:21] op_sel:[0,1] op_sel_hi:[1,0]
	v_add_u32_e32 v10, 0x1ad00, v13
	v_pk_fma_f32 v[24:25], v[24:25], v[20:21], v[26:27] op_sel_hi:[0,1,1]
	ds_write_b64 v10, v[24:25]
	v_xor_b32_e32 v24, 0x80000000, v21
	v_mov_b32_e32 v25, v21
	v_pk_mul_f32 v[24:25], v[22:23], v[24:25] op_sel:[1,0] op_sel_hi:[0,1]
	v_pk_fma_f32 v[20:21], v[22:23], v[20:21], v[24:25] op_sel_hi:[1,0,1]
	v_xor_b32_e32 v24, 0x80000000, v43
	v_mov_b32_e32 v25, v43
	v_pk_mul_f32 v[24:25], v[24:25], v[20:21] op_sel:[0,1] op_sel_hi:[1,0]
	v_add_u32_e32 v10, 0x1bd80, v13
	v_pk_fma_f32 v[24:25], v[42:43], v[20:21], v[24:25] op_sel_hi:[0,1,1]
	ds_write_b64 v10, v[24:25]
	v_xor_b32_e32 v24, 0x80000000, v21
	v_mov_b32_e32 v25, v21
	v_pk_mul_f32 v[24:25], v[22:23], v[24:25] op_sel:[1,0] op_sel_hi:[0,1]
	v_pk_fma_f32 v[20:21], v[22:23], v[20:21], v[24:25] op_sel_hi:[1,0,1]
	v_xor_b32_e32 v24, 0x80000000, v15
	v_mov_b32_e32 v25, v15
	v_pk_mul_f32 v[24:25], v[24:25], v[20:21] op_sel:[0,1] op_sel_hi:[1,0]
	v_add_u32_e32 v10, 0x1ce00, v13
	v_pk_fma_f32 v[14:15], v[14:15], v[20:21], v[24:25] op_sel_hi:[0,1,1]
	ds_write_b64 v10, v[14:15]
	v_xor_b32_e32 v14, 0x80000000, v21
	v_mov_b32_e32 v15, v21
	v_pk_mul_f32 v[14:15], v[22:23], v[14:15] op_sel:[1,0] op_sel_hi:[0,1]
	v_pk_fma_f32 v[14:15], v[22:23], v[20:21], v[14:15] op_sel_hi:[1,0,1]
	v_xor_b32_e32 v20, 0x80000000, v35
	v_mov_b32_e32 v21, v35
	v_pk_mul_f32 v[20:21], v[20:21], v[14:15] op_sel:[0,1] op_sel_hi:[1,0]
	v_add_u32_e32 v10, 0x1de80, v13
	v_pk_fma_f32 v[20:21], v[34:35], v[14:15], v[20:21] op_sel_hi:[0,1,1]
	ds_write_b64 v10, v[20:21]
	v_xor_b32_e32 v20, 0x80000000, v15
	v_mov_b32_e32 v21, v15
	v_pk_mul_f32 v[20:21], v[22:23], v[20:21] op_sel:[1,0] op_sel_hi:[0,1]
	v_pk_fma_f32 v[14:15], v[22:23], v[14:15], v[20:21] op_sel_hi:[1,0,1]
	v_xor_b32_e32 v20, 0x80000000, v19
	v_mov_b32_e32 v21, v19
	v_pk_mul_f32 v[20:21], v[20:21], v[14:15] op_sel:[0,1] op_sel_hi:[1,0]
	v_add_u32_e32 v10, 0x1ef00, v13
	v_pk_fma_f32 v[18:19], v[18:19], v[14:15], v[20:21] op_sel_hi:[0,1,1]
	ds_write_b64 v10, v[18:19]
	v_xor_b32_e32 v18, 0x80000000, v15
	v_mov_b32_e32 v19, v15
	v_pk_mul_f32 v[18:19], v[22:23], v[18:19] op_sel:[1,0] op_sel_hi:[0,1]
	v_pk_fma_f32 v[14:15], v[22:23], v[14:15], v[18:19] op_sel_hi:[1,0,1]
	v_xor_b32_e32 v18, 0x80000000, v33
	v_mov_b32_e32 v19, v33
	v_pk_mul_f32 v[18:19], v[18:19], v[14:15] op_sel:[0,1] op_sel_hi:[1,0]
	v_add_u32_e32 v10, 0x1ff80, v13
	v_pk_fma_f32 v[14:15], v[32:33], v[14:15], v[18:19] op_sel_hi:[0,1,1]
	ds_write_b64 v10, v[14:15]
	v_mov_b32_e32 v10, v174
	v_mov_b32_e32 v13, v172
	s_waitcnt lgkmcnt(0)
	s_barrier
	v_mov_b32_e32 v14, v180
	v_xad_u32 v30, v13, 3, v10
	v_lshl_add_u32 v73, v30, 3, 0
	v_xad_u32 v30, v13, 4, v10
	v_lshl_add_u32 v72, v30, 3, 0
	v_xad_u32 v30, v13, 5, v10
	v_lshl_add_u32 v71, v30, 3, 0
	v_xad_u32 v30, v13, 6, v10
	v_lshl_add_u32 v70, v30, 3, 0
	v_xad_u32 v30, v13, 7, v10
	v_lshl_add_u32 v69, v30, 3, 0
	v_xad_u32 v30, v13, 8, v10
	v_lshl_add_u32 v30, v30, 3, 0
	v_add_u32_e32 v68, 0x800, v30
	v_xad_u32 v30, v13, 9, v10
	v_lshl_add_u32 v30, v30, 3, 0
	v_add_u32_e32 v67, 0x800, v30
	v_xad_u32 v30, v13, 10, v10
	v_lshl_add_u32 v30, v30, 3, 0
	v_add_u32_e32 v66, 0x800, v30
	v_xad_u32 v30, v13, 11, v10
	v_lshl_add_u32 v30, v30, 3, 0
	v_add_u32_e32 v18, v13, v10
	v_add_u32_e32 v65, 0x800, v30
	v_xad_u32 v30, v13, 12, v10
	v_mov_b32_e32 v15, v181
	v_lshl_add_u32 v76, v18, 3, 0
	v_lshl_add_u32 v30, v30, 3, 0
	ds_read2_b64 v[18:21], v76 offset1:16
	ds_read2_b64 v[40:43], v68 offset1:16
	v_add_u32_e32 v64, 0x800, v30
	v_xad_u32 v30, v13, 13, v10
	v_xad_u32 v22, v13, 1, v10
	v_lshl_add_u32 v30, v30, 3, 0
	v_lshl_add_u32 v75, v22, 3, 0
	v_xad_u32 v26, v13, 2, v10
	v_add_u32_e32 v63, 0x800, v30
	v_xad_u32 v30, v13, 14, v10
	v_xad_u32 v10, v13, 15, v10
	ds_read2_b64 v[22:25], v75 offset0:32 offset1:48
	ds_read2_b64 v[48:51], v67 offset0:32 offset1:48
	v_lshl_add_u32 v30, v30, 3, 0
	v_lshl_add_u32 v10, v10, 3, 0
	v_lshl_add_u32 v74, v26, 3, 0
	v_add_u32_e32 v62, 0x800, v30
	v_add_u32_e32 v13, 0x800, v10
	v_mov_b32_e32 v10, v1
	ds_read2_b64 v[26:29], v74 offset0:64 offset1:80
	ds_read2_b64 v[58:61], v73 offset0:96 offset1:112
	ds_read2_b64 v[78:81], v72 offset0:128 offset1:144
	ds_read2_b64 v[82:85], v71 offset0:160 offset1:176
	ds_read2_b64 v[86:89], v70 offset0:192 offset1:208
	ds_read2_b64 v[90:93], v69 offset0:224 offset1:240
	ds_read2_b64 v[54:57], v66 offset0:64 offset1:80
	ds_read2_b64 v[94:97], v65 offset0:96 offset1:112
	ds_read2_b64 v[98:101], v64 offset0:128 offset1:144
	ds_read2_b64 v[102:105], v63 offset0:160 offset1:176
	ds_read2_b64 v[106:109], v62 offset0:192 offset1:208
	ds_read2_b64 v[110:113], v13 offset0:224 offset1:240
	s_waitcnt lgkmcnt(14)
	v_pk_add_f32 v[114:115], v[18:19], v[40:41]
	v_pk_add_f32 v[40:41], v[18:19], v[40:41] neg_lo:[0,1] neg_hi:[0,1]
	v_pk_add_f32 v[18:19], v[20:21], v[42:43]
	v_pk_add_f32 v[20:21], v[20:21], v[42:43] neg_lo:[0,1] neg_hi:[0,1]
	v_mov_b32_e32 v30, v164
	v_mov_b32_e32 v32, v165
	v_mov_b32_e32 v34, v166
	v_mov_b32_e32 v10, v167
	v_mov_b32_e32 v38, v168
	v_mov_b32_e32 v36, v169
	v_mov_b32_e32 v46, v170
	v_xor_b32_e32 v42, 0x80000000, v21
	v_mov_b32_e32 v43, v20
	v_mov_b32_e32 v31, v171
	v_pk_mul_f32 v[42:43], v[42:43], v[46:47] op_sel_hi:[1,0] neg_lo:[0,1] neg_hi:[0,1]
	s_mov_b32 s14, s95
	v_pk_fma_f32 v[44:45], v[20:21], v[30:31], v[42:43] op_sel_hi:[1,0,1]
	s_waitcnt lgkmcnt(12)
	v_pk_add_f32 v[20:21], v[22:23], v[48:49]
	v_pk_add_f32 v[22:23], v[22:23], v[48:49] neg_lo:[0,1] neg_hi:[0,1]
	s_mov_b32 s15, s94
	v_xor_b32_e32 v42, 0x80000000, v23
	v_mov_b32_e32 v43, v22
	v_pk_mul_f32 v[42:43], v[42:43], v[36:37] op_sel_hi:[1,0] neg_lo:[0,1] neg_hi:[0,1]
	s_nop 0
	v_pk_fma_f32 v[48:49], v[22:23], v[32:33], v[42:43] op_sel_hi:[1,0,1]
	v_pk_add_f32 v[22:23], v[24:25], v[50:51]
	v_pk_add_f32 v[24:25], v[24:25], v[50:51] neg_lo:[0,1] neg_hi:[0,1]
	s_nop 0
	v_xor_b32_e32 v42, 0x80000000, v25
	v_mov_b32_e32 v43, v24
	v_pk_mul_f32 v[42:43], v[42:43], v[38:39] op_sel_hi:[1,0] neg_lo:[0,1] neg_hi:[0,1]
	s_nop 0
	v_pk_fma_f32 v[52:53], v[24:25], v[34:35], v[42:43] op_sel_hi:[1,0,1]
	s_waitcnt lgkmcnt(5)
	v_pk_add_f32 v[24:25], v[26:27], v[54:55]
	v_pk_add_f32 v[26:27], v[26:27], v[54:55] neg_lo:[0,1] neg_hi:[0,1]
	s_nop 0
	v_xor_b32_e32 v42, 0x80000000, v27
	v_mov_b32_e32 v43, v26
	v_pk_mul_f32 v[42:43], v[42:43], v[10:11] op_sel_hi:[1,0] neg_lo:[0,1] neg_hi:[0,1]
	s_nop 0
	v_pk_fma_f32 v[54:55], v[26:27], v[10:11], v[42:43] op_sel_hi:[1,0,1]
	v_pk_add_f32 v[26:27], v[28:29], v[56:57]
	v_pk_add_f32 v[28:29], v[28:29], v[56:57] neg_lo:[0,1] neg_hi:[0,1]
	s_nop 0
	v_pk_mul_f32 v[42:43], v[28:29], v[38:39] op_sel_hi:[1,0]
	v_xor_b32_e32 v50, 0x80000000, v29
	v_mov_b32_e32 v51, v28
	v_pk_fma_f32 v[56:57], v[50:51], v[34:35], v[42:43] op_sel_hi:[1,0,1] neg_lo:[0,1,0] neg_hi:[0,1,0]
	s_waitcnt lgkmcnt(4)
	v_pk_add_f32 v[42:43], v[58:59], v[94:95] neg_lo:[0,1] neg_hi:[0,1]
	v_pk_add_f32 v[28:29], v[58:59], v[94:95]
	v_pk_mul_f32 v[50:51], v[42:43], v[36:37] op_sel_hi:[1,0]
	v_xor_b32_e32 v58, 0x80000000, v43
	v_mov_b32_e32 v59, v42
	v_pk_fma_f32 v[58:59], v[58:59], v[32:33], v[50:51] op_sel_hi:[1,0,1] neg_lo:[0,1,0] neg_hi:[0,1,0]
	v_pk_add_f32 v[50:51], v[60:61], v[96:97] neg_lo:[0,1] neg_hi:[0,1]
	v_pk_add_f32 v[42:43], v[60:61], v[96:97]
	v_pk_mul_f32 v[60:61], v[50:51], v[46:47] op_sel_hi:[1,0]
	v_xor_b32_e32 v94, 0x80000000, v51
	v_mov_b32_e32 v95, v50
	s_waitcnt lgkmcnt(3)
	v_pk_add_f32 v[50:51], v[78:79], v[98:99]
	v_pk_add_f32 v[78:79], v[78:79], v[98:99] neg_lo:[0,1] neg_hi:[0,1]
	v_pk_fma_f32 v[60:61], v[94:95], v[30:31], v[60:61] op_sel_hi:[1,0,1] neg_lo:[0,1,0] neg_hi:[0,1,0]
	v_xor_b32_e32 v95, 0x80000000, v78
	v_mov_b32_e32 v94, v79
	v_pk_add_f32 v[78:79], v[80:81], v[100:101]
	v_pk_add_f32 v[80:81], v[80:81], v[100:101] neg_lo:[0,1] neg_hi:[0,1]
	s_nop 0
	v_pk_mul_f32 v[96:97], v[80:81], v[46:47] op_sel_hi:[1,0] neg_lo:[0,1] neg_hi:[0,1]
	v_xor_b32_e32 v98, 0x80000000, v81
	v_mov_b32_e32 v99, v80
	v_pk_fma_f32 v[80:81], v[98:99], v[30:31], v[96:97] op_sel_hi:[1,0,1] neg_lo:[0,1,0] neg_hi:[0,1,0]
	s_waitcnt lgkmcnt(2)
	v_pk_add_f32 v[96:97], v[82:83], v[102:103]
	v_pk_add_f32 v[82:83], v[82:83], v[102:103] neg_lo:[0,1] neg_hi:[0,1]
	s_nop 0
	v_pk_mul_f32 v[98:99], v[82:83], v[36:37] op_sel_hi:[1,0] neg_lo:[0,1] neg_hi:[0,1]
	v_xor_b32_e32 v100, 0x80000000, v83
	v_mov_b32_e32 v101, v82
	v_pk_fma_f32 v[82:83], v[100:101], v[32:33], v[98:99] op_sel_hi:[1,0,1] neg_lo:[0,1,0] neg_hi:[0,1,0]
	v_pk_add_f32 v[98:99], v[84:85], v[104:105]
	v_pk_add_f32 v[84:85], v[84:85], v[104:105] neg_lo:[0,1] neg_hi:[0,1]
	s_nop 0
	v_pk_mul_f32 v[100:101], v[84:85], v[38:39] op_sel_hi:[1,0] neg_lo:[0,1] neg_hi:[0,1]
	v_xor_b32_e32 v102, 0x80000000, v85
	v_mov_b32_e32 v103, v84
	v_pk_fma_f32 v[84:85], v[102:103], v[34:35], v[100:101] op_sel_hi:[1,0,1] neg_lo:[0,1,0] neg_hi:[0,1,0]
	s_waitcnt lgkmcnt(1)
	v_pk_add_f32 v[100:101], v[86:87], v[106:107]
	v_pk_add_f32 v[86:87], v[86:87], v[106:107] neg_lo:[0,1] neg_hi:[0,1]
	s_nop 0
	v_xor_b32_e32 v102, 0x80000000, v87
	v_mov_b32_e32 v103, v86
	v_pk_mul_f32 v[102:103], v[102:103], v[10:11] op_sel_hi:[1,0] neg_lo:[0,1] neg_hi:[0,1]
	s_nop 0
	v_pk_fma_f32 v[86:87], v[86:87], v[10:11], v[102:103] op_sel_hi:[1,0,1] neg_lo:[0,1,0] neg_hi:[0,1,0]
	v_pk_add_f32 v[102:103], v[88:89], v[108:109]
	v_pk_add_f32 v[88:89], v[88:89], v[108:109] neg_lo:[0,1] neg_hi:[0,1]
	s_nop 0
	v_xor_b32_e32 v104, 0x80000000, v89
	v_mov_b32_e32 v105, v88
	v_pk_mul_f32 v[38:39], v[104:105], v[38:39] op_sel_hi:[1,0] neg_lo:[0,1] neg_hi:[0,1]
	s_nop 0
	v_pk_fma_f32 v[88:89], v[88:89], v[34:35], v[38:39] op_sel_hi:[1,0,1] neg_lo:[0,1,0] neg_hi:[0,1,0]
	s_waitcnt lgkmcnt(0)
	v_pk_add_f32 v[38:39], v[90:91], v[110:111] neg_lo:[0,1] neg_hi:[0,1]
	v_pk_add_f32 v[34:35], v[90:91], v[110:111]
	v_xor_b32_e32 v90, 0x80000000, v39
	v_mov_b32_e32 v91, v38
	v_pk_mul_f32 v[90:91], v[90:91], v[36:37] op_sel_hi:[1,0] neg_lo:[0,1] neg_hi:[0,1]
	s_nop 0
	v_pk_fma_f32 v[90:91], v[38:39], v[32:33], v[90:91] op_sel_hi:[1,0,1] neg_lo:[0,1,0] neg_hi:[0,1,0]
	v_pk_add_f32 v[38:39], v[92:93], v[112:113]
	v_pk_add_f32 v[92:93], v[92:93], v[112:113] neg_lo:[0,1] neg_hi:[0,1]
	s_nop 0
	v_xor_b32_e32 v104, 0x80000000, v93
	v_mov_b32_e32 v105, v92
	v_pk_mul_f32 v[46:47], v[104:105], v[46:47] op_sel_hi:[1,0] neg_lo:[0,1] neg_hi:[0,1]
	s_nop 0
	v_pk_fma_f32 v[92:93], v[92:93], v[30:31], v[46:47] op_sel_hi:[1,0,1] neg_lo:[0,1,0] neg_hi:[0,1,0]
	v_pk_add_f32 v[46:47], v[18:19], v[78:79]
	v_pk_add_f32 v[18:19], v[18:19], v[78:79] neg_lo:[0,1] neg_hi:[0,1]
	v_pk_add_f32 v[30:31], v[114:115], v[50:51]
	v_xor_b32_e32 v78, 0x80000000, v19
	v_mov_b32_e32 v79, v18
	v_pk_mul_f32 v[78:79], v[78:79], v[36:37] op_sel_hi:[1,0] neg_lo:[0,1] neg_hi:[0,1]
	v_pk_add_f32 v[50:51], v[114:115], v[50:51] neg_lo:[0,1] neg_hi:[0,1]
	v_pk_fma_f32 v[78:79], v[18:19], v[32:33], v[78:79] op_sel_hi:[1,0,1]
	v_pk_add_f32 v[18:19], v[20:21], v[96:97]
	v_pk_add_f32 v[20:21], v[20:21], v[96:97] neg_lo:[0,1] neg_hi:[0,1]
	s_nop 0
	v_xor_b32_e32 v96, 0x80000000, v21
	v_mov_b32_e32 v97, v20
	v_pk_mul_f32 v[96:97], v[96:97], v[10:11] op_sel_hi:[1,0] neg_lo:[0,1] neg_hi:[0,1]
	s_nop 0
	v_pk_fma_f32 v[20:21], v[20:21], v[10:11], v[96:97] op_sel_hi:[1,0,1]
	v_pk_add_f32 v[96:97], v[22:23], v[98:99]
	v_pk_add_f32 v[22:23], v[22:23], v[98:99] neg_lo:[0,1] neg_hi:[0,1]
	s_nop 0
	v_pk_mul_f32 v[98:99], v[22:23], v[36:37] op_sel_hi:[1,0]
	v_xor_b32_e32 v104, 0x80000000, v23
	v_mov_b32_e32 v105, v22
	v_pk_add_f32 v[22:23], v[24:25], v[100:101]
	v_pk_add_f32 v[24:25], v[24:25], v[100:101] neg_lo:[0,1] neg_hi:[0,1]
	v_pk_fma_f32 v[98:99], v[104:105], v[32:33], v[98:99] op_sel_hi:[1,0,1] neg_lo:[0,1,0] neg_hi:[0,1,0]
	v_xor_b32_e32 v101, 0x80000000, v24
	v_mov_b32_e32 v100, v25
	v_pk_add_f32 v[24:25], v[26:27], v[102:103]
	v_pk_add_f32 v[26:27], v[26:27], v[102:103] neg_lo:[0,1] neg_hi:[0,1]
	s_nop 0
	v_pk_mul_f32 v[102:103], v[26:27], v[36:37] op_sel_hi:[1,0] neg_lo:[0,1] neg_hi:[0,1]
	v_xor_b32_e32 v104, 0x80000000, v27
	v_mov_b32_e32 v105, v26
	v_pk_add_f32 v[26:27], v[28:29], v[34:35]
	v_pk_add_f32 v[28:29], v[28:29], v[34:35] neg_lo:[0,1] neg_hi:[0,1]
	v_pk_fma_f32 v[102:103], v[104:105], v[32:33], v[102:103] op_sel_hi:[1,0,1] neg_lo:[0,1,0] neg_hi:[0,1,0]
	v_xor_b32_e32 v34, 0x80000000, v29
	v_mov_b32_e32 v35, v28
	v_pk_mul_f32 v[34:35], v[34:35], v[10:11] op_sel_hi:[1,0] neg_lo:[0,1] neg_hi:[0,1]
	v_pk_add_f32 v[104:105], v[30:31], v[22:23] neg_lo:[0,1] neg_hi:[0,1]
	v_pk_fma_f32 v[28:29], v[28:29], v[10:11], v[34:35] op_sel_hi:[1,0,1] neg_lo:[0,1,0] neg_hi:[0,1,0]
	v_pk_add_f32 v[34:35], v[42:43], v[38:39]
	v_pk_add_f32 v[38:39], v[42:43], v[38:39] neg_lo:[0,1] neg_hi:[0,1]
	s_nop 0
	v_xor_b32_e32 v42, 0x80000000, v39
	v_mov_b32_e32 v43, v38
	v_pk_mul_f32 v[42:43], v[42:43], v[36:37] op_sel_hi:[1,0] neg_lo:[0,1] neg_hi:[0,1]
	s_nop 0
	v_pk_fma_f32 v[42:43], v[38:39], v[32:33], v[42:43] op_sel_hi:[1,0,1] neg_lo:[0,1,0] neg_hi:[0,1,0]
	v_pk_add_f32 v[38:39], v[30:31], v[22:23]
	v_pk_add_f32 v[22:23], v[46:47], v[24:25]
	v_pk_add_f32 v[24:25], v[46:47], v[24:25] neg_lo:[0,1] neg_hi:[0,1]
	s_nop 0
	v_xor_b32_e32 v30, 0x80000000, v25
	v_mov_b32_e32 v31, v24
	v_pk_mul_f32 v[30:31], v[30:31], v[10:11] op_sel_hi:[1,0] neg_lo:[0,1] neg_hi:[0,1]
	s_nop 0
	v_pk_fma_f32 v[24:25], v[24:25], v[10:11], v[30:31] op_sel_hi:[1,0,1]
	v_pk_add_f32 v[30:31], v[18:19], v[26:27]
	v_pk_add_f32 v[18:19], v[18:19], v[26:27] neg_lo:[0,1] neg_hi:[0,1]
	s_nop 0
	v_xor_b32_e32 v27, 0x80000000, v18
	v_mov_b32_e32 v26, v19
	v_pk_add_f32 v[18:19], v[96:97], v[34:35]
	v_pk_add_f32 v[34:35], v[96:97], v[34:35] neg_lo:[0,1] neg_hi:[0,1]
	s_nop 0
	v_xor_b32_e32 v46, 0x80000000, v35
	v_mov_b32_e32 v47, v34
	v_pk_mul_f32 v[46:47], v[46:47], v[10:11] op_sel_hi:[1,0] neg_lo:[0,1] neg_hi:[0,1]
	s_nop 0
	v_pk_fma_f32 v[34:35], v[34:35], v[10:11], v[46:47] op_sel_hi:[1,0,1] neg_lo:[0,1,0] neg_hi:[0,1,0]
	v_pk_add_f32 v[46:47], v[38:39], v[30:31]
	v_pk_add_f32 v[38:39], v[38:39], v[30:31] neg_lo:[0,1] neg_hi:[0,1]
	v_pk_add_f32 v[30:31], v[22:23], v[18:19]
	v_pk_add_f32 v[18:19], v[22:23], v[18:19] neg_lo:[0,1] neg_hi:[0,1]
	v_pk_add_f32 v[96:97], v[46:47], v[30:31]
	v_xor_b32_e32 v23, 0x80000000, v18
	v_mov_b32_e32 v22, v19
	v_pk_add_f32 v[18:19], v[104:105], v[26:27]
	v_pk_add_f32 v[104:105], v[104:105], v[26:27] neg_lo:[0,1] neg_hi:[0,1]
	v_pk_add_f32 v[26:27], v[24:25], v[34:35]
	v_pk_add_f32 v[24:25], v[24:25], v[34:35] neg_lo:[0,1] neg_hi:[0,1]
	v_pk_add_f32 v[30:31], v[46:47], v[30:31] neg_lo:[0,1] neg_hi:[0,1]
	v_xor_b32_e32 v35, 0x80000000, v24
	v_mov_b32_e32 v34, v25
	v_pk_add_f32 v[24:25], v[50:51], v[100:101]
	v_pk_add_f32 v[100:101], v[50:51], v[100:101] neg_lo:[0,1] neg_hi:[0,1]
	v_pk_add_f32 v[50:51], v[78:79], v[102:103] neg_lo:[0,1] neg_hi:[0,1]
	v_pk_add_f32 v[46:47], v[38:39], v[22:23]
	v_pk_add_f32 v[22:23], v[38:39], v[22:23] neg_lo:[0,1] neg_hi:[0,1]
	v_pk_add_f32 v[106:107], v[18:19], v[26:27]
	v_pk_add_f32 v[26:27], v[18:19], v[26:27] neg_lo:[0,1] neg_hi:[0,1]
	v_pk_add_f32 v[38:39], v[104:105], v[34:35]
	v_pk_add_f32 v[18:19], v[104:105], v[34:35] neg_lo:[0,1] neg_hi:[0,1]
	v_pk_add_f32 v[34:35], v[78:79], v[102:103]
	v_xor_b32_e32 v78, 0x80000000, v51
	v_mov_b32_e32 v79, v50
	v_pk_mul_f32 v[78:79], v[10:11], v[78:79] op_sel_hi:[0,1] neg_lo:[1,0] neg_hi:[1,0]
	v_pk_fma_f32 v[78:79], v[10:11], v[50:51], v[78:79] op_sel_hi:[0,1,1]
	v_pk_add_f32 v[50:51], v[20:21], v[28:29]
	v_pk_add_f32 v[20:21], v[20:21], v[28:29] neg_lo:[0,1] neg_hi:[0,1]
	s_nop 0
	v_xor_b32_e32 v29, 0x80000000, v20
	v_mov_b32_e32 v28, v21
	v_pk_add_f32 v[20:21], v[98:99], v[42:43]
	v_pk_add_f32 v[42:43], v[98:99], v[42:43] neg_lo:[0,1] neg_hi:[0,1]
	s_nop 0
	v_xor_b32_e32 v98, 0x80000000, v43
	v_mov_b32_e32 v99, v42
	v_pk_mul_f32 v[98:99], v[10:11], v[98:99] op_sel_hi:[0,1] neg_lo:[1,0] neg_hi:[1,0]
	v_pk_fma_f32 v[42:43], v[10:11], v[42:43], v[98:99] op_sel_hi:[0,1,1] neg_lo:[1,0,0] neg_hi:[1,0,0]
	v_pk_add_f32 v[98:99], v[24:25], v[50:51]
	v_pk_add_f32 v[24:25], v[24:25], v[50:51] neg_lo:[0,1] neg_hi:[0,1]
	v_pk_add_f32 v[50:51], v[34:35], v[20:21]
	v_pk_add_f32 v[20:21], v[34:35], v[20:21] neg_lo:[0,1] neg_hi:[0,1]
	v_pk_add_f32 v[104:105], v[98:99], v[50:51]
	v_xor_b32_e32 v103, 0x80000000, v20
	v_mov_b32_e32 v102, v21
	v_pk_add_f32 v[34:35], v[98:99], v[50:51] neg_lo:[0,1] neg_hi:[0,1]
	v_pk_add_f32 v[20:21], v[100:101], v[28:29]
	v_pk_add_f32 v[98:99], v[100:101], v[28:29] neg_lo:[0,1] neg_hi:[0,1]
	v_pk_add_f32 v[28:29], v[78:79], v[42:43]
	v_pk_add_f32 v[42:43], v[78:79], v[42:43] neg_lo:[0,1] neg_hi:[0,1]
	v_pk_add_f32 v[100:101], v[20:21], v[28:29]
	v_xor_b32_e32 v79, 0x80000000, v42
	v_mov_b32_e32 v78, v43
	v_pk_add_f32 v[28:29], v[20:21], v[28:29] neg_lo:[0,1] neg_hi:[0,1]
	v_pk_add_f32 v[42:43], v[98:99], v[78:79]
	v_pk_add_f32 v[20:21], v[98:99], v[78:79] neg_lo:[0,1] neg_hi:[0,1]
	v_pk_add_f32 v[78:79], v[40:41], v[94:95]
	v_pk_add_f32 v[94:95], v[40:41], v[94:95] neg_lo:[0,1] neg_hi:[0,1]
	v_pk_add_f32 v[40:41], v[44:45], v[80:81]
	v_pk_add_f32 v[44:45], v[44:45], v[80:81] neg_lo:[0,1] neg_hi:[0,1]
	v_pk_add_f32 v[50:51], v[24:25], v[102:103]
	v_xor_b32_e32 v80, 0x80000000, v45
	v_mov_b32_e32 v81, v44
	v_pk_mul_f32 v[80:81], v[36:37], v[80:81] op_sel_hi:[0,1] neg_lo:[1,0] neg_hi:[1,0]
	v_pk_fma_f32 v[44:45], v[32:33], v[44:45], v[80:81] op_sel_hi:[0,1,1]
	v_pk_add_f32 v[80:81], v[48:49], v[82:83]
	v_pk_add_f32 v[48:49], v[48:49], v[82:83] neg_lo:[0,1] neg_hi:[0,1]
	v_pk_add_f32 v[24:25], v[24:25], v[102:103] neg_lo:[0,1] neg_hi:[0,1]
	v_xor_b32_e32 v82, 0x80000000, v49
	v_mov_b32_e32 v83, v48
	v_pk_mul_f32 v[82:83], v[10:11], v[82:83] op_sel_hi:[0,1] neg_lo:[1,0] neg_hi:[1,0]
	v_pk_fma_f32 v[82:83], v[10:11], v[48:49], v[82:83] op_sel_hi:[0,1,1]
	v_pk_add_f32 v[48:49], v[52:53], v[84:85]
	v_pk_add_f32 v[52:53], v[52:53], v[84:85] neg_lo:[0,1] neg_hi:[0,1]
	s_nop 0
	v_xor_b32_e32 v84, 0x80000000, v53
	v_mov_b32_e32 v85, v52
	v_pk_mul_f32 v[84:85], v[32:33], v[84:85] op_sel_hi:[0,1] neg_lo:[1,0] neg_hi:[1,0]
	v_pk_fma_f32 v[52:53], v[36:37], v[52:53], v[84:85] op_sel_hi:[0,1,1]
	v_pk_add_f32 v[84:85], v[54:55], v[86:87]
	v_pk_add_f32 v[54:55], v[54:55], v[86:87] neg_lo:[0,1] neg_hi:[0,1]
	s_nop 0
	v_xor_b32_e32 v87, 0x80000000, v54
	v_mov_b32_e32 v86, v55
	v_pk_add_f32 v[54:55], v[56:57], v[88:89]
	v_pk_add_f32 v[56:57], v[56:57], v[88:89] neg_lo:[0,1] neg_hi:[0,1]
	s_nop 0
	v_xor_b32_e32 v88, 0x80000000, v57
	v_mov_b32_e32 v89, v56
	v_pk_mul_f32 v[88:89], v[32:33], v[88:89] op_sel_hi:[0,1] neg_lo:[1,0] neg_hi:[1,0]
	v_pk_fma_f32 v[56:57], v[36:37], v[56:57], v[88:89] op_sel_hi:[0,1,1] neg_lo:[1,0,0] neg_hi:[1,0,0]
	v_pk_add_f32 v[88:89], v[58:59], v[90:91]
	v_pk_add_f32 v[58:59], v[58:59], v[90:91] neg_lo:[0,1] neg_hi:[0,1]
	s_nop 0
	v_xor_b32_e32 v90, 0x80000000, v59
	v_mov_b32_e32 v91, v58
	v_pk_mul_f32 v[90:91], v[10:11], v[90:91] op_sel_hi:[0,1] neg_lo:[1,0] neg_hi:[1,0]
	v_pk_fma_f32 v[58:59], v[10:11], v[58:59], v[90:91] op_sel_hi:[0,1,1] neg_lo:[1,0,0] neg_hi:[1,0,0]
	v_pk_add_f32 v[90:91], v[60:61], v[92:93]
	v_pk_add_f32 v[60:61], v[60:61], v[92:93] neg_lo:[0,1] neg_hi:[0,1]
	s_nop 0
	v_xor_b32_e32 v92, 0x80000000, v61
	v_mov_b32_e32 v93, v60
	v_pk_mul_f32 v[36:37], v[36:37], v[92:93] op_sel_hi:[0,1] neg_lo:[1,0] neg_hi:[1,0]
	v_pk_fma_f32 v[36:37], v[32:33], v[60:61], v[36:37] op_sel_hi:[0,1,1] neg_lo:[1,0,0] neg_hi:[1,0,0]
	v_pk_add_f32 v[32:33], v[78:79], v[84:85]
	v_pk_add_f32 v[60:61], v[78:79], v[84:85] neg_lo:[0,1] neg_hi:[0,1]
	v_pk_add_f32 v[78:79], v[54:55], v[40:41]
	v_pk_add_f32 v[40:41], v[40:41], v[54:55] neg_lo:[0,1] neg_hi:[0,1]
	s_nop 0
	v_xor_b32_e32 v54, 0x80000000, v41
	v_mov_b32_e32 v55, v40
	v_pk_mul_f32 v[54:55], v[10:11], v[54:55] op_sel_hi:[0,1] neg_lo:[1,0] neg_hi:[1,0]
	v_pk_fma_f32 v[54:55], v[10:11], v[40:41], v[54:55] op_sel_hi:[0,1,1]
	v_pk_add_f32 v[40:41], v[80:81], v[88:89]
	v_pk_add_f32 v[80:81], v[80:81], v[88:89] neg_lo:[0,1] neg_hi:[0,1]
	s_nop 0
	v_xor_b32_e32 v85, 0x80000000, v80
	v_mov_b32_e32 v84, v81
	v_pk_add_f32 v[80:81], v[48:49], v[90:91]
	v_pk_add_f32 v[48:49], v[48:49], v[90:91] neg_lo:[0,1] neg_hi:[0,1]
	v_pk_add_f32 v[90:91], v[78:79], v[80:81]
	v_xor_b32_e32 v88, 0x80000000, v49
	v_mov_b32_e32 v89, v48
	v_pk_mul_f32 v[88:89], v[10:11], v[88:89] op_sel_hi:[0,1] neg_lo:[1,0] neg_hi:[1,0]
	v_pk_fma_f32 v[48:49], v[10:11], v[48:49], v[88:89] op_sel_hi:[0,1,1] neg_lo:[1,0,0] neg_hi:[1,0,0]
	v_pk_add_f32 v[88:89], v[32:33], v[40:41]
	v_pk_add_f32 v[32:33], v[32:33], v[40:41] neg_lo:[0,1] neg_hi:[0,1]
	v_pk_add_f32 v[40:41], v[78:79], v[80:81] neg_lo:[0,1] neg_hi:[0,1]
	v_pk_add_f32 v[80:81], v[88:89], v[90:91] neg_lo:[0,1] neg_hi:[0,1]
	v_xor_b32_e32 v79, 0x80000000, v40
	v_mov_b32_e32 v78, v41
	v_pk_add_f32 v[92:93], v[32:33], v[78:79]
	v_pk_add_f32 v[40:41], v[32:33], v[78:79] neg_lo:[0,1] neg_hi:[0,1]
	v_pk_add_f32 v[78:79], v[54:55], v[48:49]
	v_pk_add_f32 v[48:49], v[54:55], v[48:49] neg_lo:[0,1] neg_hi:[0,1]
	v_pk_add_f32 v[32:33], v[60:61], v[84:85]
	v_pk_add_f32 v[60:61], v[60:61], v[84:85] neg_lo:[0,1] neg_hi:[0,1]
	v_xor_b32_e32 v55, 0x80000000, v48
	v_mov_b32_e32 v54, v49
	v_pk_add_f32 v[84:85], v[32:33], v[78:79]
	v_pk_add_f32 v[48:49], v[32:33], v[78:79] neg_lo:[0,1] neg_hi:[0,1]
	v_pk_add_f32 v[78:79], v[60:61], v[54:55]
	v_pk_add_f32 v[32:33], v[60:61], v[54:55] neg_lo:[0,1] neg_hi:[0,1]
	v_pk_add_f32 v[54:55], v[94:95], v[86:87]
	v_pk_add_f32 v[60:61], v[94:95], v[86:87] neg_lo:[0,1] neg_hi:[0,1]
	v_pk_add_f32 v[86:87], v[56:57], v[44:45]
	v_pk_add_f32 v[44:45], v[44:45], v[56:57] neg_lo:[0,1] neg_hi:[0,1]
	v_pk_add_f32 v[88:89], v[88:89], v[90:91]
	v_xor_b32_e32 v56, 0x80000000, v45
	v_mov_b32_e32 v57, v44
	v_pk_mul_f32 v[56:57], v[10:11], v[56:57] op_sel_hi:[0,1] neg_lo:[1,0] neg_hi:[1,0]
	v_pk_fma_f32 v[56:57], v[10:11], v[44:45], v[56:57] op_sel_hi:[0,1,1]
	v_pk_add_f32 v[44:45], v[82:83], v[58:59]
	v_pk_add_f32 v[58:59], v[82:83], v[58:59] neg_lo:[0,1] neg_hi:[0,1]
	v_xor_b32_e32 v90, 0x80000000, v89
	v_xor_b32_e32 v83, 0x80000000, v58
	v_mov_b32_e32 v82, v59
	v_pk_add_f32 v[58:59], v[52:53], v[36:37]
	v_pk_add_f32 v[36:37], v[52:53], v[36:37] neg_lo:[0,1] neg_hi:[0,1]
	v_mov_b32_e32 v91, v89
	v_xor_b32_e32 v52, 0x80000000, v37
	v_mov_b32_e32 v53, v36
	v_pk_mul_f32 v[52:53], v[10:11], v[52:53] op_sel_hi:[0,1] neg_lo:[1,0] neg_hi:[1,0]
	v_pk_fma_f32 v[36:37], v[10:11], v[36:37], v[52:53] op_sel_hi:[0,1,1] neg_lo:[1,0,0] neg_hi:[1,0,0]
	v_pk_add_f32 v[52:53], v[54:55], v[44:45]
	v_pk_add_f32 v[44:45], v[54:55], v[44:45] neg_lo:[0,1] neg_hi:[0,1]
	v_pk_add_f32 v[54:55], v[86:87], v[58:59]
	v_pk_add_f32 v[58:59], v[86:87], v[58:59] neg_lo:[0,1] neg_hi:[0,1]
	s_nop 0
	v_xor_b32_e32 v87, 0x80000000, v58
	v_mov_b32_e32 v86, v59
	v_pk_add_f32 v[58:59], v[52:53], v[54:55]
	v_pk_add_f32 v[54:55], v[52:53], v[54:55] neg_lo:[0,1] neg_hi:[0,1]
	v_pk_add_f32 v[52:53], v[60:61], v[82:83]
	v_pk_add_f32 v[60:61], v[60:61], v[82:83] neg_lo:[0,1] neg_hi:[0,1]
	v_pk_add_f32 v[82:83], v[56:57], v[36:37]
	v_pk_add_f32 v[36:37], v[56:57], v[36:37] neg_lo:[0,1] neg_hi:[0,1]
	v_pk_add_f32 v[94:95], v[44:45], v[86:87]
	v_xor_b32_e32 v57, 0x80000000, v36
	v_mov_b32_e32 v56, v37
	v_pk_add_f32 v[44:45], v[44:45], v[86:87] neg_lo:[0,1] neg_hi:[0,1]
	v_pk_add_f32 v[86:87], v[52:53], v[82:83]
	v_pk_add_f32 v[52:53], v[52:53], v[82:83] neg_lo:[0,1] neg_hi:[0,1]
	v_pk_add_f32 v[82:83], v[60:61], v[56:57]
	v_pk_add_f32 v[36:37], v[60:61], v[56:57] neg_lo:[0,1] neg_hi:[0,1]
	v_xor_b32_e32 v56, 0x80000000, v97
	v_mov_b32_e32 v57, v97
	v_pk_fma_f32 v[60:61], v[14:15], s[90:91], v[14:15] op_sel:[1,0,0] op_sel_hi:[0,1,1]
	v_pk_mul_f32 v[56:57], v[56:57], s[14:15]
	v_pk_mul_f32 v[90:91], v[60:61], v[90:91] op_sel:[1,0] op_sel_hi:[0,1]
	v_pk_fma_f32 v[56:57], v[96:97], s[94:95], v[56:57] op_sel_hi:[0,1,1]
	v_pk_fma_f32 v[88:89], v[60:61], v[88:89], v[90:91] op_sel_hi:[1,0,1]
	ds_write2_b64 v76, v[56:57], v[88:89] offset1:16
	v_xor_b32_e32 v56, 0x80000000, v61
	v_mov_b32_e32 v57, v61
	v_pk_mul_f32 v[56:57], v[14:15], v[56:57] op_sel:[1,0] op_sel_hi:[0,1]
	v_pk_fma_f32 v[56:57], v[14:15], v[60:61], v[56:57] op_sel_hi:[1,0,1]
	v_xor_b32_e32 v60, 0x80000000, v105
	v_mov_b32_e32 v61, v105
	v_xor_b32_e32 v76, 0x80000000, v57
	v_mov_b32_e32 v77, v57
	v_pk_mul_f32 v[60:61], v[56:57], v[60:61] op_sel:[1,0] op_sel_hi:[0,1]
	v_pk_mul_f32 v[76:77], v[14:15], v[76:77] op_sel:[1,0] op_sel_hi:[0,1]
	v_pk_fma_f32 v[60:61], v[56:57], v[104:105], v[60:61] op_sel_hi:[1,0,1]
	v_pk_fma_f32 v[56:57], v[14:15], v[56:57], v[76:77] op_sel_hi:[1,0,1]
	v_xor_b32_e32 v76, 0x80000000, v59
	v_mov_b32_e32 v77, v59
	v_pk_mul_f32 v[76:77], v[56:57], v[76:77] op_sel:[1,0] op_sel_hi:[0,1]
	v_pk_fma_f32 v[58:59], v[56:57], v[58:59], v[76:77] op_sel_hi:[1,0,1]
	ds_write2_b64 v75, v[60:61], v[58:59] offset0:32 offset1:48
	v_xor_b32_e32 v58, 0x80000000, v57
	v_mov_b32_e32 v59, v57
	v_pk_mul_f32 v[58:59], v[14:15], v[58:59] op_sel:[1,0] op_sel_hi:[0,1]
	v_pk_fma_f32 v[56:57], v[14:15], v[56:57], v[58:59] op_sel_hi:[1,0,1]
	v_xor_b32_e32 v58, 0x80000000, v107
	v_mov_b32_e32 v59, v107
	v_xor_b32_e32 v60, 0x80000000, v57
	v_mov_b32_e32 v61, v57
	v_pk_mul_f32 v[58:59], v[56:57], v[58:59] op_sel:[1,0] op_sel_hi:[0,1]
	v_pk_mul_f32 v[60:61], v[14:15], v[60:61] op_sel:[1,0] op_sel_hi:[0,1]
	v_pk_fma_f32 v[58:59], v[56:57], v[106:107], v[58:59] op_sel_hi:[1,0,1]
	v_pk_fma_f32 v[56:57], v[14:15], v[56:57], v[60:61] op_sel_hi:[1,0,1]
	v_xor_b32_e32 v60, 0x80000000, v85
	v_mov_b32_e32 v61, v85
	v_pk_mul_f32 v[60:61], v[56:57], v[60:61] op_sel:[1,0] op_sel_hi:[0,1]
	v_pk_fma_f32 v[60:61], v[56:57], v[84:85], v[60:61] op_sel_hi:[1,0,1]
	ds_write2_b64 v74, v[58:59], v[60:61] offset0:64 offset1:80
	v_xor_b32_e32 v58, 0x80000000, v57
	v_mov_b32_e32 v59, v57
	v_pk_mul_f32 v[58:59], v[14:15], v[58:59] op_sel:[1,0] op_sel_hi:[0,1]
	v_pk_fma_f32 v[56:57], v[14:15], v[56:57], v[58:59] op_sel_hi:[1,0,1]
	v_xor_b32_e32 v58, 0x80000000, v101
	v_mov_b32_e32 v59, v101
	v_xor_b32_e32 v60, 0x80000000, v57
	v_mov_b32_e32 v61, v57
	v_pk_mul_f32 v[58:59], v[56:57], v[58:59] op_sel:[1,0] op_sel_hi:[0,1]
	v_pk_mul_f32 v[60:61], v[14:15], v[60:61] op_sel:[1,0] op_sel_hi:[0,1]
	v_pk_fma_f32 v[58:59], v[56:57], v[100:101], v[58:59] op_sel_hi:[1,0,1]
	v_pk_fma_f32 v[56:57], v[14:15], v[56:57], v[60:61] op_sel_hi:[1,0,1]
	v_xor_b32_e32 v60, 0x80000000, v87
	v_mov_b32_e32 v61, v87
	v_pk_mul_f32 v[60:61], v[56:57], v[60:61] op_sel:[1,0] op_sel_hi:[0,1]
	v_pk_fma_f32 v[60:61], v[56:57], v[86:87], v[60:61] op_sel_hi:[1,0,1]
	ds_write2_b64 v73, v[58:59], v[60:61] offset0:96 offset1:112
	v_xor_b32_e32 v58, 0x80000000, v57
	v_mov_b32_e32 v59, v57
	v_pk_mul_f32 v[58:59], v[14:15], v[58:59] op_sel:[1,0] op_sel_hi:[0,1]
	v_pk_fma_f32 v[56:57], v[14:15], v[56:57], v[58:59] op_sel_hi:[1,0,1]
	v_xor_b32_e32 v58, 0x80000000, v47
	v_mov_b32_e32 v59, v47
	v_pk_mul_f32 v[58:59], v[56:57], v[58:59] op_sel:[1,0] op_sel_hi:[0,1]
	v_pk_fma_f32 v[46:47], v[56:57], v[46:47], v[58:59] op_sel_hi:[1,0,1]
	v_xor_b32_e32 v58, 0x80000000, v57
	v_mov_b32_e32 v59, v57
	v_pk_mul_f32 v[58:59], v[14:15], v[58:59] op_sel:[1,0] op_sel_hi:[0,1]
	v_pk_fma_f32 v[56:57], v[14:15], v[56:57], v[58:59] op_sel_hi:[1,0,1]
	v_xor_b32_e32 v58, 0x80000000, v93
	v_mov_b32_e32 v59, v93
	v_pk_mul_f32 v[58:59], v[56:57], v[58:59] op_sel:[1,0] op_sel_hi:[0,1]
	v_pk_fma_f32 v[58:59], v[56:57], v[92:93], v[58:59] op_sel_hi:[1,0,1]
	ds_write2_b64 v72, v[46:47], v[58:59] offset0:128 offset1:144
	v_xor_b32_e32 v46, 0x80000000, v57
	v_mov_b32_e32 v47, v57
	v_pk_mul_f32 v[46:47], v[14:15], v[46:47] op_sel:[1,0] op_sel_hi:[0,1]
	v_pk_fma_f32 v[46:47], v[14:15], v[56:57], v[46:47] op_sel_hi:[1,0,1]
	v_xor_b32_e32 v56, 0x80000000, v51
	v_mov_b32_e32 v57, v51
	v_pk_mul_f32 v[56:57], v[46:47], v[56:57] op_sel:[1,0] op_sel_hi:[0,1]
	v_pk_fma_f32 v[50:51], v[46:47], v[50:51], v[56:57] op_sel_hi:[1,0,1]
	v_xor_b32_e32 v56, 0x80000000, v47
	v_mov_b32_e32 v57, v47
	v_pk_mul_f32 v[56:57], v[14:15], v[56:57] op_sel:[1,0] op_sel_hi:[0,1]
	v_pk_fma_f32 v[46:47], v[14:15], v[46:47], v[56:57] op_sel_hi:[1,0,1]
	v_xor_b32_e32 v56, 0x80000000, v95
	v_mov_b32_e32 v57, v95
	v_pk_mul_f32 v[56:57], v[46:47], v[56:57] op_sel:[1,0] op_sel_hi:[0,1]
	v_pk_fma_f32 v[56:57], v[46:47], v[94:95], v[56:57] op_sel_hi:[1,0,1]
	ds_write2_b64 v71, v[50:51], v[56:57] offset0:160 offset1:176
	v_xor_b32_e32 v50, 0x80000000, v47
	v_mov_b32_e32 v51, v47
	v_pk_mul_f32 v[50:51], v[14:15], v[50:51] op_sel:[1,0] op_sel_hi:[0,1]
	v_pk_fma_f32 v[46:47], v[14:15], v[46:47], v[50:51] op_sel_hi:[1,0,1]
	v_xor_b32_e32 v50, 0x80000000, v39
	v_mov_b32_e32 v51, v39
	v_pk_mul_f32 v[50:51], v[50:51], v[46:47] op_sel:[0,1] op_sel_hi:[1,0]
	s_nop 0
	v_pk_fma_f32 v[38:39], v[38:39], v[46:47], v[50:51] op_sel_hi:[0,1,1]
	v_xor_b32_e32 v50, 0x80000000, v47
	v_mov_b32_e32 v51, v47
	v_pk_mul_f32 v[50:51], v[14:15], v[50:51] op_sel:[1,0] op_sel_hi:[0,1]
	v_pk_fma_f32 v[46:47], v[14:15], v[46:47], v[50:51] op_sel_hi:[1,0,1]
	v_xor_b32_e32 v50, 0x80000000, v79
	v_mov_b32_e32 v51, v79
	v_pk_mul_f32 v[50:51], v[46:47], v[50:51] op_sel:[1,0] op_sel_hi:[0,1]
	v_pk_fma_f32 v[50:51], v[46:47], v[78:79], v[50:51] op_sel_hi:[1,0,1]
	ds_write2_b64 v70, v[38:39], v[50:51] offset0:192 offset1:208
	v_xor_b32_e32 v38, 0x80000000, v47
	v_mov_b32_e32 v39, v47
	v_pk_mul_f32 v[38:39], v[14:15], v[38:39] op_sel:[1,0] op_sel_hi:[0,1]
	v_pk_fma_f32 v[38:39], v[14:15], v[46:47], v[38:39] op_sel_hi:[1,0,1]
	v_xor_b32_e32 v46, 0x80000000, v43
	v_mov_b32_e32 v47, v43
	v_pk_mul_f32 v[46:47], v[46:47], v[38:39] op_sel:[0,1] op_sel_hi:[1,0]
	s_nop 0
	v_pk_fma_f32 v[42:43], v[42:43], v[38:39], v[46:47] op_sel_hi:[0,1,1]
	v_xor_b32_e32 v46, 0x80000000, v39
	v_mov_b32_e32 v47, v39
	v_pk_mul_f32 v[46:47], v[14:15], v[46:47] op_sel:[1,0] op_sel_hi:[0,1]
	v_pk_fma_f32 v[38:39], v[14:15], v[38:39], v[46:47] op_sel_hi:[1,0,1]
	v_xor_b32_e32 v46, 0x80000000, v83
	v_mov_b32_e32 v47, v83
	v_pk_mul_f32 v[46:47], v[38:39], v[46:47] op_sel:[1,0] op_sel_hi:[0,1]
	v_pk_fma_f32 v[46:47], v[38:39], v[82:83], v[46:47] op_sel_hi:[1,0,1]
	ds_write2_b64 v69, v[42:43], v[46:47] offset0:224 offset1:240
	v_xor_b32_e32 v42, 0x80000000, v39
	v_mov_b32_e32 v43, v39
	v_pk_mul_f32 v[42:43], v[14:15], v[42:43] op_sel:[1,0] op_sel_hi:[0,1]
	v_pk_fma_f32 v[38:39], v[14:15], v[38:39], v[42:43] op_sel_hi:[1,0,1]
	v_xor_b32_e32 v42, 0x80000000, v31
	v_mov_b32_e32 v43, v31
	v_pk_mul_f32 v[42:43], v[42:43], v[38:39] op_sel:[0,1] op_sel_hi:[1,0]
	s_nop 0
	v_pk_fma_f32 v[30:31], v[30:31], v[38:39], v[42:43] op_sel_hi:[0,1,1]
	v_xor_b32_e32 v42, 0x80000000, v39
	v_mov_b32_e32 v43, v39
	v_pk_mul_f32 v[42:43], v[14:15], v[42:43] op_sel:[1,0] op_sel_hi:[0,1]
	v_pk_fma_f32 v[38:39], v[14:15], v[38:39], v[42:43] op_sel_hi:[1,0,1]
	v_xor_b32_e32 v42, 0x80000000, v81
	v_mov_b32_e32 v43, v81
	v_pk_mul_f32 v[42:43], v[42:43], v[38:39] op_sel:[0,1] op_sel_hi:[1,0]
	s_nop 0
	v_pk_fma_f32 v[42:43], v[80:81], v[38:39], v[42:43] op_sel_hi:[0,1,1]
	ds_write2_b64 v68, v[30:31], v[42:43] offset1:16
	v_xor_b32_e32 v30, 0x80000000, v39
	v_mov_b32_e32 v31, v39
	v_pk_mul_f32 v[30:31], v[14:15], v[30:31] op_sel:[1,0] op_sel_hi:[0,1]
	v_pk_fma_f32 v[30:31], v[14:15], v[38:39], v[30:31] op_sel_hi:[1,0,1]
	v_xor_b32_e32 v38, 0x80000000, v35
	v_mov_b32_e32 v39, v35
	v_pk_mul_f32 v[38:39], v[38:39], v[30:31] op_sel:[0,1] op_sel_hi:[1,0]
	s_nop 0
	v_pk_fma_f32 v[34:35], v[34:35], v[30:31], v[38:39] op_sel_hi:[0,1,1]
	v_xor_b32_e32 v38, 0x80000000, v31
	v_mov_b32_e32 v39, v31
	v_pk_mul_f32 v[38:39], v[14:15], v[38:39] op_sel:[1,0] op_sel_hi:[0,1]
	v_pk_fma_f32 v[30:31], v[14:15], v[30:31], v[38:39] op_sel_hi:[1,0,1]
	v_xor_b32_e32 v38, 0x80000000, v55
	v_mov_b32_e32 v39, v55
	v_pk_mul_f32 v[38:39], v[38:39], v[30:31] op_sel:[0,1] op_sel_hi:[1,0]
	s_nop 0
	v_pk_fma_f32 v[38:39], v[54:55], v[30:31], v[38:39] op_sel_hi:[0,1,1]
	ds_write2_b64 v67, v[34:35], v[38:39] offset0:32 offset1:48
	v_xor_b32_e32 v34, 0x80000000, v31
	v_mov_b32_e32 v35, v31
	v_pk_mul_f32 v[34:35], v[14:15], v[34:35] op_sel:[1,0] op_sel_hi:[0,1]
	v_pk_fma_f32 v[30:31], v[14:15], v[30:31], v[34:35] op_sel_hi:[1,0,1]
	v_xor_b32_e32 v34, 0x80000000, v27
	v_mov_b32_e32 v35, v27
	v_pk_mul_f32 v[34:35], v[34:35], v[30:31] op_sel:[0,1] op_sel_hi:[1,0]
	s_nop 0
	v_pk_fma_f32 v[26:27], v[26:27], v[30:31], v[34:35] op_sel_hi:[0,1,1]
	v_xor_b32_e32 v34, 0x80000000, v31
	v_mov_b32_e32 v35, v31
	v_pk_mul_f32 v[34:35], v[14:15], v[34:35] op_sel:[1,0] op_sel_hi:[0,1]
	v_pk_fma_f32 v[30:31], v[14:15], v[30:31], v[34:35] op_sel_hi:[1,0,1]
	v_xor_b32_e32 v34, 0x80000000, v49
	v_mov_b32_e32 v35, v49
	v_pk_mul_f32 v[34:35], v[34:35], v[30:31] op_sel:[0,1] op_sel_hi:[1,0]
	s_nop 0
	v_pk_fma_f32 v[34:35], v[48:49], v[30:31], v[34:35] op_sel_hi:[0,1,1]
	ds_write2_b64 v66, v[26:27], v[34:35] offset0:64 offset1:80
	v_xor_b32_e32 v26, 0x80000000, v31
	v_mov_b32_e32 v27, v31
	v_pk_mul_f32 v[26:27], v[14:15], v[26:27] op_sel:[1,0] op_sel_hi:[0,1]
	v_pk_fma_f32 v[26:27], v[14:15], v[30:31], v[26:27] op_sel_hi:[1,0,1]
	v_xor_b32_e32 v30, 0x80000000, v29
	v_mov_b32_e32 v31, v29
	v_pk_mul_f32 v[30:31], v[30:31], v[26:27] op_sel:[0,1] op_sel_hi:[1,0]
	s_nop 0
	v_pk_fma_f32 v[28:29], v[28:29], v[26:27], v[30:31] op_sel_hi:[0,1,1]
	v_xor_b32_e32 v30, 0x80000000, v27
	v_mov_b32_e32 v31, v27
	v_pk_mul_f32 v[30:31], v[14:15], v[30:31] op_sel:[1,0] op_sel_hi:[0,1]
	v_pk_fma_f32 v[26:27], v[14:15], v[26:27], v[30:31] op_sel_hi:[1,0,1]
	v_xor_b32_e32 v30, 0x80000000, v53
	v_mov_b32_e32 v31, v53
	v_pk_mul_f32 v[30:31], v[30:31], v[26:27] op_sel:[0,1] op_sel_hi:[1,0]
	s_nop 0
	v_pk_fma_f32 v[30:31], v[52:53], v[26:27], v[30:31] op_sel_hi:[0,1,1]
	ds_write2_b64 v65, v[28:29], v[30:31] offset0:96 offset1:112
	v_xor_b32_e32 v28, 0x80000000, v27
	v_mov_b32_e32 v29, v27
	v_pk_mul_f32 v[28:29], v[14:15], v[28:29] op_sel:[1,0] op_sel_hi:[0,1]
	v_pk_fma_f32 v[26:27], v[14:15], v[26:27], v[28:29] op_sel_hi:[1,0,1]
	v_xor_b32_e32 v28, 0x80000000, v23
	v_mov_b32_e32 v29, v23
	v_pk_mul_f32 v[28:29], v[28:29], v[26:27] op_sel:[0,1] op_sel_hi:[1,0]
	s_nop 0
	v_pk_fma_f32 v[22:23], v[22:23], v[26:27], v[28:29] op_sel_hi:[0,1,1]
	v_xor_b32_e32 v28, 0x80000000, v27
	v_mov_b32_e32 v29, v27
	v_pk_mul_f32 v[28:29], v[14:15], v[28:29] op_sel:[1,0] op_sel_hi:[0,1]
	v_pk_fma_f32 v[26:27], v[14:15], v[26:27], v[28:29] op_sel_hi:[1,0,1]
	v_xor_b32_e32 v28, 0x80000000, v41
	v_mov_b32_e32 v29, v41
	v_pk_mul_f32 v[28:29], v[28:29], v[26:27] op_sel:[0,1] op_sel_hi:[1,0]
	s_nop 0
	v_pk_fma_f32 v[28:29], v[40:41], v[26:27], v[28:29] op_sel_hi:[0,1,1]
	ds_write2_b64 v64, v[22:23], v[28:29] offset0:128 offset1:144
	v_xor_b32_e32 v22, 0x80000000, v27
	v_mov_b32_e32 v23, v27
	v_pk_mul_f32 v[22:23], v[14:15], v[22:23] op_sel:[1,0] op_sel_hi:[0,1]
	v_pk_fma_f32 v[22:23], v[14:15], v[26:27], v[22:23] op_sel_hi:[1,0,1]
	v_xor_b32_e32 v26, 0x80000000, v25
	v_mov_b32_e32 v27, v25
	v_pk_mul_f32 v[26:27], v[26:27], v[22:23] op_sel:[0,1] op_sel_hi:[1,0]
	s_nop 0
	v_pk_fma_f32 v[24:25], v[24:25], v[22:23], v[26:27] op_sel_hi:[0,1,1]
	v_xor_b32_e32 v26, 0x80000000, v23
	v_mov_b32_e32 v27, v23
	v_pk_mul_f32 v[26:27], v[14:15], v[26:27] op_sel:[1,0] op_sel_hi:[0,1]
	v_pk_fma_f32 v[22:23], v[14:15], v[22:23], v[26:27] op_sel_hi:[1,0,1]
	v_xor_b32_e32 v26, 0x80000000, v45
	v_mov_b32_e32 v27, v45
	v_pk_mul_f32 v[26:27], v[26:27], v[22:23] op_sel:[0,1] op_sel_hi:[1,0]
	s_nop 0
	v_pk_fma_f32 v[26:27], v[44:45], v[22:23], v[26:27] op_sel_hi:[0,1,1]
	ds_write2_b64 v63, v[24:25], v[26:27] offset0:160 offset1:176
	v_xor_b32_e32 v24, 0x80000000, v23
	v_mov_b32_e32 v25, v23
	v_pk_mul_f32 v[24:25], v[14:15], v[24:25] op_sel:[1,0] op_sel_hi:[0,1]
	v_pk_fma_f32 v[22:23], v[14:15], v[22:23], v[24:25] op_sel_hi:[1,0,1]
	v_xor_b32_e32 v24, 0x80000000, v19
	v_mov_b32_e32 v25, v19
	v_pk_mul_f32 v[24:25], v[24:25], v[22:23] op_sel:[0,1] op_sel_hi:[1,0]
	s_nop 0
	v_pk_fma_f32 v[18:19], v[18:19], v[22:23], v[24:25] op_sel_hi:[0,1,1]
	v_xor_b32_e32 v24, 0x80000000, v23
	v_mov_b32_e32 v25, v23
	v_pk_mul_f32 v[24:25], v[14:15], v[24:25] op_sel:[1,0] op_sel_hi:[0,1]
	v_pk_fma_f32 v[22:23], v[14:15], v[22:23], v[24:25] op_sel_hi:[1,0,1]
	v_xor_b32_e32 v24, 0x80000000, v33
	v_mov_b32_e32 v25, v33
	v_pk_mul_f32 v[24:25], v[24:25], v[22:23] op_sel:[0,1] op_sel_hi:[1,0]
	s_nop 0
	v_pk_fma_f32 v[24:25], v[32:33], v[22:23], v[24:25] op_sel_hi:[0,1,1]
	ds_write2_b64 v62, v[18:19], v[24:25] offset0:192 offset1:208
	v_xor_b32_e32 v18, 0x80000000, v23
	v_mov_b32_e32 v19, v23
	v_pk_mul_f32 v[18:19], v[14:15], v[18:19] op_sel:[1,0] op_sel_hi:[0,1]
	v_pk_fma_f32 v[18:19], v[14:15], v[22:23], v[18:19] op_sel_hi:[1,0,1]
	v_xor_b32_e32 v22, 0x80000000, v21
	v_mov_b32_e32 v23, v21
	v_pk_mul_f32 v[22:23], v[22:23], v[18:19] op_sel:[0,1] op_sel_hi:[1,0]
	s_nop 0
	v_pk_fma_f32 v[20:21], v[20:21], v[18:19], v[22:23] op_sel_hi:[0,1,1]
	v_xor_b32_e32 v22, 0x80000000, v19
	v_mov_b32_e32 v23, v19
	v_pk_mul_f32 v[22:23], v[14:15], v[22:23] op_sel:[1,0] op_sel_hi:[0,1]
	v_pk_fma_f32 v[14:15], v[14:15], v[18:19], v[22:23] op_sel_hi:[1,0,1]
	v_xor_b32_e32 v18, 0x80000000, v37
	v_mov_b32_e32 v19, v37
	v_pk_mul_f32 v[18:19], v[18:19], v[14:15] op_sel:[0,1] op_sel_hi:[1,0]
	s_nop 0
	v_pk_fma_f32 v[14:15], v[36:37], v[14:15], v[18:19] op_sel_hi:[0,1,1]
	ds_write2_b64 v13, v[20:21], v[14:15] offset0:224 offset1:240
	v_mov_b32_e32 v14, v182
	v_mov_b32_e32 v10, v176
	v_mov_b32_e32 v13, v175
	s_waitcnt lgkmcnt(0)
	s_barrier
	v_mov_b32_e32 v50, v167
	v_xor_b32_e32 v18, 1, v13
	v_lshlrev_b32_e32 v10, 3, v10
	v_lshlrev_b32_e32 v18, 3, v18
	v_add3_u32 v20, 0, v18, v10
	v_xor_b32_e32 v18, 2, v13
	v_lshlrev_b32_e32 v18, 3, v18
	v_xor_b32_e32 v26, 5, v13
	v_add3_u32 v22, 0, v18, v10
	v_xor_b32_e32 v18, 3, v13
	v_lshlrev_b32_e32 v26, 3, v26
	v_lshlrev_b32_e32 v15, 3, v13
	v_lshlrev_b32_e32 v18, 3, v18
	v_add3_u32 v28, 0, v26, v10
	v_xor_b32_e32 v26, 6, v13
	v_add3_u32 v15, 0, v15, v10
	v_add3_u32 v24, 0, v18, v10
	v_lshlrev_b32_e32 v26, 3, v26
	v_xor_b32_e32 v34, 9, v13
	ds_read_b64 v[18:19], v15
	ds_read_b64 v[20:21], v20
	ds_read_b64 v[22:23], v22
	ds_read_b64 v[24:25], v24
	v_xor_b32_e32 v15, 4, v13
	v_add3_u32 v30, 0, v26, v10
	v_xor_b32_e32 v26, 7, v13
	v_lshlrev_b32_e32 v34, 3, v34
	v_lshlrev_b32_e32 v15, 3, v15
	v_lshlrev_b32_e32 v26, 3, v26
	v_add3_u32 v36, 0, v34, v10
	v_xor_b32_e32 v34, 10, v13
	v_add3_u32 v15, 0, v15, v10
	v_add3_u32 v32, 0, v26, v10
	v_lshlrev_b32_e32 v34, 3, v34
	ds_read_b64 v[26:27], v15
	ds_read_b64 v[28:29], v28
	ds_read_b64 v[30:31], v30
	ds_read_b64 v[32:33], v32
	v_xor_b32_e32 v15, 8, v13
	v_add3_u32 v38, 0, v34, v10
	v_xor_b32_e32 v34, 11, v13
	v_lshlrev_b32_e32 v15, 3, v15
	v_lshlrev_b32_e32 v34, 3, v34
	v_xor_b32_e32 v42, 13, v13
	v_add3_u32 v15, 0, v15, v10
	v_add3_u32 v40, 0, v34, v10
	v_lshlrev_b32_e32 v42, 3, v42
	ds_read_b64 v[34:35], v15
	ds_read_b64 v[36:37], v36
	ds_read_b64 v[38:39], v38
	ds_read_b64 v[40:41], v40
	v_xor_b32_e32 v15, 12, v13
	v_add3_u32 v44, 0, v42, v10
	v_xor_b32_e32 v42, 14, v13
	v_xor_b32_e32 v13, 15, v13
	v_lshlrev_b32_e32 v15, 3, v15
	v_lshlrev_b32_e32 v42, 3, v42
	v_lshlrev_b32_e32 v13, 3, v13
	v_add3_u32 v15, 0, v15, v10
	v_add3_u32 v46, 0, v42, v10
	v_add3_u32 v10, 0, v13, v10
	ds_read_b64 v[42:43], v15
	ds_read_b64 v[44:45], v44
	ds_read_b64 v[46:47], v46
	ds_read_b64 v[48:49], v10
	v_mov_b32_e32 v10, v1
	v_mov_b32_e32 v13, v166
	v_mov_b32_e32 v10, v164
	s_waitcnt lgkmcnt(7)
	v_pk_add_f32 v[54:55], v[18:19], v[34:35]
	v_mov_b32_e32 v10, v165
	v_pk_add_f32 v[18:19], v[18:19], v[34:35] neg_lo:[0,1] neg_hi:[0,1]
	s_waitcnt lgkmcnt(6)
	v_pk_add_f32 v[34:35], v[20:21], v[36:37]
	v_pk_add_f32 v[20:21], v[20:21], v[36:37] neg_lo:[0,1] neg_hi:[0,1]
	v_mov_b32_e32 v13, v168
	v_mov_b32_e32 v52, v169
	v_xor_b32_e32 v36, 0x80000000, v21
	v_mov_b32_e32 v37, v20
	v_ashrrev_i32_e32 v15, 31, v14
	v_pk_mul_f32 v[36:37], v[36:37], v[52:53] op_sel_hi:[1,0] neg_lo:[0,1] neg_hi:[0,1]
	v_mov_b32_e32 v13, v170
	v_pk_fma_f32 v[20:21], v[20:21], v[10:11], v[36:37] op_sel_hi:[1,0,1]
	s_waitcnt lgkmcnt(5)
	v_pk_add_f32 v[36:37], v[22:23], v[38:39]
	v_pk_add_f32 v[22:23], v[22:23], v[38:39] neg_lo:[0,1] neg_hi:[0,1]
	s_movk_i32 s0, 0x1000
	v_xor_b32_e32 v38, 0x80000000, v23
	v_mov_b32_e32 v39, v22
	v_pk_mul_f32 v[38:39], v[38:39], v[50:51] op_sel_hi:[1,0] neg_lo:[0,1] neg_hi:[0,1]
	v_mov_b32_e32 v13, v171
	v_pk_fma_f32 v[22:23], v[22:23], v[50:51], v[38:39] op_sel_hi:[1,0,1]
	s_waitcnt lgkmcnt(4)
	v_pk_add_f32 v[38:39], v[24:25], v[40:41]
	v_pk_add_f32 v[24:25], v[24:25], v[40:41] neg_lo:[0,1] neg_hi:[0,1]
	v_mov_b32_e32 v72, v164
	v_pk_mul_f32 v[40:41], v[24:25], v[52:53] op_sel_hi:[1,0]
	v_xor_b32_e32 v56, 0x80000000, v25
	v_mov_b32_e32 v57, v24
	v_pk_fma_f32 v[24:25], v[56:57], v[10:11], v[40:41] op_sel_hi:[1,0,1] neg_lo:[0,1,0] neg_hi:[0,1,0]
	s_waitcnt lgkmcnt(3)
	v_pk_add_f32 v[40:41], v[26:27], v[42:43]
	v_pk_add_f32 v[26:27], v[26:27], v[42:43] neg_lo:[0,1] neg_hi:[0,1]
	v_mov_b32_e32 v13, v175
	v_xor_b32_e32 v43, 0x80000000, v26
	v_mov_b32_e32 v42, v27
	s_waitcnt lgkmcnt(2)
	v_pk_add_f32 v[26:27], v[28:29], v[44:45]
	v_pk_add_f32 v[28:29], v[28:29], v[44:45] neg_lo:[0,1] neg_hi:[0,1]
	v_mov_b32_e32 v74, v166
	v_pk_mul_f32 v[44:45], v[28:29], v[52:53] op_sel_hi:[1,0] neg_lo:[0,1] neg_hi:[0,1]
	v_xor_b32_e32 v56, 0x80000000, v29
	v_mov_b32_e32 v57, v28
	v_pk_fma_f32 v[28:29], v[56:57], v[10:11], v[44:45] op_sel_hi:[1,0,1] neg_lo:[0,1,0] neg_hi:[0,1,0]
	s_waitcnt lgkmcnt(1)
	v_pk_add_f32 v[44:45], v[30:31], v[46:47]
	v_pk_add_f32 v[30:31], v[30:31], v[46:47] neg_lo:[0,1] neg_hi:[0,1]
	v_mov_b32_e32 v76, v168
	v_xor_b32_e32 v46, 0x80000000, v31
	v_mov_b32_e32 v47, v30
	v_pk_mul_f32 v[46:47], v[46:47], v[50:51] op_sel_hi:[1,0] neg_lo:[0,1] neg_hi:[0,1]
	v_mov_b32_e32 v78, v170
	v_pk_fma_f32 v[30:31], v[30:31], v[50:51], v[46:47] op_sel_hi:[1,0,1] neg_lo:[0,1,0] neg_hi:[0,1,0]
	s_waitcnt lgkmcnt(0)
	v_pk_add_f32 v[46:47], v[32:33], v[48:49]
	v_pk_add_f32 v[32:33], v[32:33], v[48:49] neg_lo:[0,1] neg_hi:[0,1]
	v_mov_b32_e32 v83, v11
	v_xor_b32_e32 v48, 0x80000000, v33
	v_mov_b32_e32 v49, v32
	v_pk_mul_f32 v[48:49], v[48:49], v[52:53] op_sel_hi:[1,0] neg_lo:[0,1] neg_hi:[0,1]
	v_pk_add_f32 v[52:53], v[34:35], v[26:27]
	v_pk_add_f32 v[26:27], v[34:35], v[26:27] neg_lo:[0,1] neg_hi:[0,1]
	v_pk_fma_f32 v[32:33], v[32:33], v[10:11], v[48:49] op_sel_hi:[1,0,1] neg_lo:[0,1,0] neg_hi:[0,1,0]
	v_xor_b32_e32 v34, 0x80000000, v27
	v_mov_b32_e32 v35, v26
	v_pk_mul_f32 v[34:35], v[34:35], v[50:51] op_sel_hi:[1,0] neg_lo:[0,1] neg_hi:[0,1]
	v_pk_add_f32 v[48:49], v[54:55], v[40:41]
	v_pk_fma_f32 v[26:27], v[26:27], v[50:51], v[34:35] op_sel_hi:[1,0,1]
	v_pk_add_f32 v[34:35], v[36:37], v[44:45]
	v_pk_add_f32 v[36:37], v[36:37], v[44:45] neg_lo:[0,1] neg_hi:[0,1]
	v_pk_add_f32 v[40:41], v[54:55], v[40:41] neg_lo:[0,1] neg_hi:[0,1]
	v_xor_b32_e32 v45, 0x80000000, v36
	v_mov_b32_e32 v44, v37
	v_pk_add_f32 v[36:37], v[38:39], v[46:47]
	v_pk_add_f32 v[38:39], v[38:39], v[46:47] neg_lo:[0,1] neg_hi:[0,1]
	v_mov_b32_e32 v10, v177
	v_xor_b32_e32 v46, 0x80000000, v39
	v_mov_b32_e32 v47, v38
	v_pk_mul_f32 v[46:47], v[46:47], v[50:51] op_sel_hi:[1,0] neg_lo:[0,1] neg_hi:[0,1]
	s_mov_b32 s7, 0xa000
	v_pk_fma_f32 v[38:39], v[38:39], v[50:51], v[46:47] op_sel_hi:[1,0,1] neg_lo:[0,1,0] neg_hi:[0,1,0]
	v_pk_add_f32 v[46:47], v[48:49], v[34:35]
	v_pk_add_f32 v[34:35], v[48:49], v[34:35] neg_lo:[0,1] neg_hi:[0,1]
	v_pk_add_f32 v[48:49], v[52:53], v[36:37]
	v_pk_add_f32 v[36:37], v[52:53], v[36:37] neg_lo:[0,1] neg_hi:[0,1]
	s_mov_b32 s6, 0xc000
	v_xor_b32_e32 v53, 0x80000000, v36
	v_mov_b32_e32 v52, v37
	v_pk_add_f32 v[36:37], v[46:47], v[48:49]
	v_pk_add_f32 v[46:47], v[46:47], v[48:49] neg_lo:[0,1] neg_hi:[0,1]
	v_pk_add_f32 v[48:49], v[34:35], v[52:53]
	v_pk_add_f32 v[34:35], v[34:35], v[52:53] neg_lo:[0,1] neg_hi:[0,1]
	v_pk_add_f32 v[52:53], v[40:41], v[44:45]
	v_pk_add_f32 v[40:41], v[40:41], v[44:45] neg_lo:[0,1] neg_hi:[0,1]
	v_pk_add_f32 v[44:45], v[26:27], v[38:39]
	v_pk_add_f32 v[26:27], v[26:27], v[38:39] neg_lo:[0,1] neg_hi:[0,1]
	s_mov_b32 s1, 0xe000
	v_xor_b32_e32 v39, 0x80000000, v26
	v_mov_b32_e32 v38, v27
	v_pk_add_f32 v[26:27], v[52:53], v[44:45]
	v_pk_add_f32 v[44:45], v[52:53], v[44:45] neg_lo:[0,1] neg_hi:[0,1]
	v_pk_add_f32 v[52:53], v[40:41], v[38:39]
	v_pk_add_f32 v[38:39], v[40:41], v[38:39] neg_lo:[0,1] neg_hi:[0,1]
	v_pk_add_f32 v[40:41], v[18:19], v[42:43]
	v_pk_add_f32 v[18:19], v[18:19], v[42:43] neg_lo:[0,1] neg_hi:[0,1]
	v_pk_add_f32 v[42:43], v[20:21], v[28:29]
	v_pk_add_f32 v[20:21], v[20:21], v[28:29] neg_lo:[0,1] neg_hi:[0,1]
	s_mov_b32 s8, 0x8000
	v_xor_b32_e32 v28, 0x80000000, v21
	v_mov_b32_e32 v29, v20
	v_pk_mul_f32 v[28:29], v[50:51], v[28:29] op_sel_hi:[0,1] neg_lo:[1,0] neg_hi:[1,0]
	v_pk_fma_f32 v[20:21], v[50:51], v[20:21], v[28:29] op_sel_hi:[0,1,1]
	v_pk_add_f32 v[28:29], v[22:23], v[30:31]
	v_pk_add_f32 v[22:23], v[22:23], v[30:31] neg_lo:[0,1] neg_hi:[0,1]
	s_mov_b32 s9, 0x9000
	v_xor_b32_e32 v31, 0x80000000, v22
	v_mov_b32_e32 v30, v23
	v_pk_add_f32 v[22:23], v[24:25], v[32:33]
	v_pk_add_f32 v[24:25], v[24:25], v[32:33] neg_lo:[0,1] neg_hi:[0,1]
	s_mov_b32 s5, 0xb000
	v_xor_b32_e32 v32, 0x80000000, v25
	v_mov_b32_e32 v33, v24
	v_pk_mul_f32 v[32:33], v[50:51], v[32:33] op_sel_hi:[0,1] neg_lo:[1,0] neg_hi:[1,0]
	v_pk_fma_f32 v[24:25], v[50:51], v[24:25], v[32:33] op_sel_hi:[0,1,1] neg_lo:[1,0,0] neg_hi:[1,0,0]
	v_pk_add_f32 v[32:33], v[40:41], v[28:29]
	v_pk_add_f32 v[28:29], v[40:41], v[28:29] neg_lo:[0,1] neg_hi:[0,1]
	v_pk_add_f32 v[40:41], v[42:43], v[22:23]
	v_pk_add_f32 v[22:23], v[42:43], v[22:23] neg_lo:[0,1] neg_hi:[0,1]
	v_mov_b32_e32 v50, v167
	v_xor_b32_e32 v43, 0x80000000, v22
	v_mov_b32_e32 v42, v23
	v_pk_add_f32 v[22:23], v[32:33], v[40:41]
	v_pk_add_f32 v[32:33], v[32:33], v[40:41] neg_lo:[0,1] neg_hi:[0,1]
	v_pk_add_f32 v[40:41], v[28:29], v[42:43]
	v_pk_add_f32 v[28:29], v[28:29], v[42:43] neg_lo:[0,1] neg_hi:[0,1]
	v_pk_add_f32 v[42:43], v[18:19], v[30:31]
	v_pk_add_f32 v[18:19], v[18:19], v[30:31] neg_lo:[0,1] neg_hi:[0,1]
	v_pk_add_f32 v[30:31], v[20:21], v[24:25]
	v_pk_add_f32 v[20:21], v[20:21], v[24:25] neg_lo:[0,1] neg_hi:[0,1]
	s_mov_b32 s4, 0xd000
	v_xor_b32_e32 v25, 0x80000000, v20
	v_mov_b32_e32 v24, v21
	v_pk_add_f32 v[20:21], v[42:43], v[30:31]
	v_pk_add_f32 v[30:31], v[42:43], v[30:31] neg_lo:[0,1] neg_hi:[0,1]
	v_pk_add_f32 v[42:43], v[18:19], v[24:25]
	v_pk_add_f32 v[18:19], v[18:19], v[24:25] neg_lo:[0,1] neg_hi:[0,1]
	v_lshl_add_u64 v[24:25], v[14:15], 3, s[46:47]
	global_store_dwordx2 v[24:25], v[36:37], off
	v_add_u32_e32 v24, 0x200, v14
	v_ashrrev_i32_e32 v25, 31, v24
	v_lshl_add_u64 v[24:25], v[24:25], 3, s[46:47]
	global_store_dwordx2 v[24:25], v[22:23], off
	v_add_u32_e32 v22, 0x400, v14
	v_ashrrev_i32_e32 v23, 31, v22
	v_lshl_add_u64 v[22:23], v[22:23], 3, s[46:47]
	global_store_dwordx2 v[22:23], v[26:27], off
	v_add_u32_e32 v22, 0x600, v14
	v_ashrrev_i32_e32 v23, 31, v22
	v_lshl_add_u64 v[22:23], v[22:23], 3, s[46:47]
	global_store_dwordx2 v[22:23], v[20:21], off
	v_add_u32_e32 v20, 0x800, v14
	v_ashrrev_i32_e32 v21, 31, v20
	v_lshl_add_u64 v[20:21], v[20:21], 3, s[46:47]
	global_store_dwordx2 v[20:21], v[48:49], off
	v_add_u32_e32 v20, 0xa00, v14
	v_ashrrev_i32_e32 v21, 31, v20
	v_lshl_add_u64 v[20:21], v[20:21], 3, s[46:47]
	global_store_dwordx2 v[20:21], v[40:41], off
	v_add_u32_e32 v20, 0xc00, v14
	v_ashrrev_i32_e32 v21, 31, v20
	v_lshl_add_u64 v[20:21], v[20:21], 3, s[46:47]
	global_store_dwordx2 v[20:21], v[52:53], off
	v_add_u32_e32 v20, 0xe00, v14
	v_ashrrev_i32_e32 v21, 31, v20
	v_lshl_add_u64 v[20:21], v[20:21], 3, s[46:47]
	global_store_dwordx2 v[20:21], v[42:43], off
	v_add_u32_e32 v20, 0x1000, v14
	v_ashrrev_i32_e32 v21, 31, v20
	v_lshl_add_u64 v[20:21], v[20:21], 3, s[46:47]
	global_store_dwordx2 v[20:21], v[46:47], off
	v_add_u32_e32 v20, 0x1200, v14
	v_ashrrev_i32_e32 v21, 31, v20
	v_lshl_add_u64 v[20:21], v[20:21], 3, s[46:47]
	global_store_dwordx2 v[20:21], v[32:33], off
	v_add_u32_e32 v20, 0x1400, v14
	v_ashrrev_i32_e32 v21, 31, v20
	v_lshl_add_u64 v[20:21], v[20:21], 3, s[46:47]
	global_store_dwordx2 v[20:21], v[44:45], off
	v_add_u32_e32 v20, 0x1600, v14
	v_ashrrev_i32_e32 v21, 31, v20
	v_lshl_add_u64 v[20:21], v[20:21], 3, s[46:47]
	global_store_dwordx2 v[20:21], v[30:31], off
	v_add_u32_e32 v20, 0x1800, v14
	v_ashrrev_i32_e32 v21, 31, v20
	v_lshl_add_u64 v[20:21], v[20:21], 3, s[46:47]
	global_store_dwordx2 v[20:21], v[34:35], off
	v_add_u32_e32 v20, 0x1a00, v14
	v_ashrrev_i32_e32 v21, 31, v20
	v_lshl_add_u64 v[20:21], v[20:21], 3, s[46:47]
	global_store_dwordx2 v[20:21], v[28:29], off
	v_add_u32_e32 v20, 0x1c00, v14
	v_ashrrev_i32_e32 v21, 31, v20
	v_lshl_add_u64 v[20:21], v[20:21], 3, s[46:47]
	global_store_dwordx2 v[20:21], v[38:39], off
	v_add_u32_e32 v20, 0x1e00, v14
	v_ashrrev_i32_e32 v21, 31, v20
	v_lshl_add_u64 v[20:21], v[20:21], 3, s[46:47]
	global_store_dwordx2 v[20:21], v[18:19], off
	v_mov_b32_e32 v52, v169
	v_xor_b32_e32 v18, 1, v13
	v_lshlrev_b32_e32 v10, 3, v10
	v_lshlrev_b32_e32 v18, 3, v18
	v_add3_u32 v20, 0, v18, v10
	v_xor_b32_e32 v18, 2, v13
	v_lshlrev_b32_e32 v18, 3, v18
	v_xor_b32_e32 v26, 5, v13
	v_add3_u32 v22, 0, v18, v10
	v_xor_b32_e32 v18, 3, v13
	v_lshlrev_b32_e32 v26, 3, v26
	v_lshlrev_b32_e32 v15, 3, v13
	v_lshlrev_b32_e32 v18, 3, v18
	v_add3_u32 v28, 0, v26, v10
	v_xor_b32_e32 v26, 6, v13
	v_add3_u32 v15, 0, v15, v10
	v_add3_u32 v24, 0, v18, v10
	v_lshlrev_b32_e32 v26, 3, v26
	v_xor_b32_e32 v34, 9, v13
	ds_read_b64 v[18:19], v15
	ds_read_b64 v[20:21], v20
	ds_read_b64 v[22:23], v22
	ds_read_b64 v[24:25], v24
	v_xor_b32_e32 v15, 4, v13
	v_add3_u32 v30, 0, v26, v10
	v_xor_b32_e32 v26, 7, v13
	v_lshlrev_b32_e32 v34, 3, v34
	v_lshlrev_b32_e32 v15, 3, v15
	v_lshlrev_b32_e32 v26, 3, v26
	v_add3_u32 v36, 0, v34, v10
	v_xor_b32_e32 v34, 10, v13
	v_add3_u32 v15, 0, v15, v10
	v_add3_u32 v32, 0, v26, v10
	v_lshlrev_b32_e32 v34, 3, v34
	ds_read_b64 v[26:27], v15
	ds_read_b64 v[28:29], v28
	ds_read_b64 v[30:31], v30
	ds_read_b64 v[32:33], v32
	v_xor_b32_e32 v15, 8, v13
	v_add3_u32 v38, 0, v34, v10
	v_xor_b32_e32 v34, 11, v13
	v_lshlrev_b32_e32 v15, 3, v15
	v_lshlrev_b32_e32 v34, 3, v34
	v_xor_b32_e32 v42, 13, v13
	v_add3_u32 v15, 0, v15, v10
	v_add3_u32 v40, 0, v34, v10
	v_lshlrev_b32_e32 v42, 3, v42
	ds_read_b64 v[34:35], v15
	ds_read_b64 v[36:37], v36
	ds_read_b64 v[38:39], v38
	ds_read_b64 v[40:41], v40
	v_xor_b32_e32 v15, 12, v13
	v_add3_u32 v44, 0, v42, v10
	v_xor_b32_e32 v42, 14, v13
	v_xor_b32_e32 v13, 15, v13
	v_lshlrev_b32_e32 v15, 3, v15
	v_lshlrev_b32_e32 v42, 3, v42
	v_lshlrev_b32_e32 v13, 3, v13
	v_add3_u32 v15, 0, v15, v10
	v_add3_u32 v46, 0, v42, v10
	v_add3_u32 v10, 0, v13, v10
	ds_read_b64 v[42:43], v15
	ds_read_b64 v[44:45], v44
	ds_read_b64 v[46:47], v46
	ds_read_b64 v[48:49], v10
	v_mov_b32_e32 v10, v1
	v_mov_b32_e32 v13, v166
	v_mov_b32_e32 v10, v164
	s_waitcnt lgkmcnt(7)
	v_pk_add_f32 v[54:55], v[18:19], v[34:35]
	v_mov_b32_e32 v10, v165
	v_pk_add_f32 v[18:19], v[18:19], v[34:35] neg_lo:[0,1] neg_hi:[0,1]
	s_waitcnt lgkmcnt(6)
	v_pk_add_f32 v[34:35], v[20:21], v[36:37]
	v_pk_add_f32 v[20:21], v[20:21], v[36:37] neg_lo:[0,1] neg_hi:[0,1]
	v_mov_b32_e32 v13, v168
	v_xor_b32_e32 v36, 0x80000000, v21
	v_mov_b32_e32 v37, v20
	s_nop 0
	v_pk_mul_f32 v[36:37], v[36:37], v[52:53] op_sel_hi:[1,0] neg_lo:[0,1] neg_hi:[0,1]
	v_mov_b32_e32 v13, v170
	v_pk_fma_f32 v[20:21], v[20:21], v[10:11], v[36:37] op_sel_hi:[1,0,1]
	s_waitcnt lgkmcnt(5)
	v_pk_add_f32 v[36:37], v[22:23], v[38:39]
	v_pk_add_f32 v[22:23], v[22:23], v[38:39] neg_lo:[0,1] neg_hi:[0,1]
	s_nop 0
	v_xor_b32_e32 v38, 0x80000000, v23
	v_mov_b32_e32 v39, v22
	v_pk_mul_f32 v[38:39], v[38:39], v[50:51] op_sel_hi:[1,0] neg_lo:[0,1] neg_hi:[0,1]
	v_mov_b32_e32 v13, v171
	v_pk_fma_f32 v[22:23], v[22:23], v[50:51], v[38:39] op_sel_hi:[1,0,1]
	s_waitcnt lgkmcnt(4)
	v_pk_add_f32 v[38:39], v[24:25], v[40:41]
	v_pk_add_f32 v[24:25], v[24:25], v[40:41] neg_lo:[0,1] neg_hi:[0,1]
	s_nop 0
	v_pk_mul_f32 v[40:41], v[24:25], v[52:53] op_sel_hi:[1,0]
	v_xor_b32_e32 v56, 0x80000000, v25
	v_mov_b32_e32 v57, v24
	v_pk_fma_f32 v[24:25], v[56:57], v[10:11], v[40:41] op_sel_hi:[1,0,1] neg_lo:[0,1,0] neg_hi:[0,1,0]
	s_waitcnt lgkmcnt(3)
	v_pk_add_f32 v[40:41], v[26:27], v[42:43]
	v_pk_add_f32 v[26:27], v[26:27], v[42:43] neg_lo:[0,1] neg_hi:[0,1]
	s_nop 0
	v_xor_b32_e32 v43, 0x80000000, v26
	v_mov_b32_e32 v42, v27
	s_waitcnt lgkmcnt(2)
	v_pk_add_f32 v[26:27], v[28:29], v[44:45]
	v_pk_add_f32 v[28:29], v[28:29], v[44:45] neg_lo:[0,1] neg_hi:[0,1]
	s_nop 0
	v_pk_mul_f32 v[44:45], v[28:29], v[52:53] op_sel_hi:[1,0] neg_lo:[0,1] neg_hi:[0,1]
	v_xor_b32_e32 v56, 0x80000000, v29
	v_mov_b32_e32 v57, v28
	v_pk_fma_f32 v[28:29], v[56:57], v[10:11], v[44:45] op_sel_hi:[1,0,1] neg_lo:[0,1,0] neg_hi:[0,1,0]
	s_waitcnt lgkmcnt(1)
	v_pk_add_f32 v[44:45], v[30:31], v[46:47]
	v_pk_add_f32 v[30:31], v[30:31], v[46:47] neg_lo:[0,1] neg_hi:[0,1]
	s_nop 0
	v_xor_b32_e32 v46, 0x80000000, v31
	v_mov_b32_e32 v47, v30
	v_pk_mul_f32 v[46:47], v[46:47], v[50:51] op_sel_hi:[1,0] neg_lo:[0,1] neg_hi:[0,1]
	s_nop 0
	v_pk_fma_f32 v[30:31], v[30:31], v[50:51], v[46:47] op_sel_hi:[1,0,1] neg_lo:[0,1,0] neg_hi:[0,1,0]
	s_waitcnt lgkmcnt(0)
	v_pk_add_f32 v[46:47], v[32:33], v[48:49]
	v_pk_add_f32 v[32:33], v[32:33], v[48:49] neg_lo:[0,1] neg_hi:[0,1]
	s_nop 0
	v_xor_b32_e32 v48, 0x80000000, v33
	v_mov_b32_e32 v49, v32
	v_pk_mul_f32 v[48:49], v[48:49], v[52:53] op_sel_hi:[1,0] neg_lo:[0,1] neg_hi:[0,1]
	v_pk_add_f32 v[52:53], v[34:35], v[26:27]
	v_pk_add_f32 v[26:27], v[34:35], v[26:27] neg_lo:[0,1] neg_hi:[0,1]
	v_pk_fma_f32 v[32:33], v[32:33], v[10:11], v[48:49] op_sel_hi:[1,0,1] neg_lo:[0,1,0] neg_hi:[0,1,0]
	v_xor_b32_e32 v34, 0x80000000, v27
	v_mov_b32_e32 v35, v26
	v_pk_mul_f32 v[34:35], v[34:35], v[50:51] op_sel_hi:[1,0] neg_lo:[0,1] neg_hi:[0,1]
	v_pk_add_f32 v[48:49], v[54:55], v[40:41]
	v_pk_fma_f32 v[26:27], v[26:27], v[50:51], v[34:35] op_sel_hi:[1,0,1]
	v_pk_add_f32 v[34:35], v[36:37], v[44:45]
	v_pk_add_f32 v[36:37], v[36:37], v[44:45] neg_lo:[0,1] neg_hi:[0,1]
	v_pk_add_f32 v[40:41], v[54:55], v[40:41] neg_lo:[0,1] neg_hi:[0,1]
	v_xor_b32_e32 v45, 0x80000000, v36
	v_mov_b32_e32 v44, v37
	v_pk_add_f32 v[36:37], v[38:39], v[46:47]
	v_pk_add_f32 v[38:39], v[38:39], v[46:47] neg_lo:[0,1] neg_hi:[0,1]
	v_mov_b32_e32 v10, v1
	v_xor_b32_e32 v46, 0x80000000, v39
	v_mov_b32_e32 v47, v38
	v_pk_mul_f32 v[46:47], v[46:47], v[50:51] op_sel_hi:[1,0] neg_lo:[0,1] neg_hi:[0,1]
	s_nop 0
	v_pk_fma_f32 v[38:39], v[38:39], v[50:51], v[46:47] op_sel_hi:[1,0,1] neg_lo:[0,1,0] neg_hi:[0,1,0]
	v_pk_add_f32 v[46:47], v[48:49], v[34:35]
	v_pk_add_f32 v[34:35], v[48:49], v[34:35] neg_lo:[0,1] neg_hi:[0,1]
	v_pk_add_f32 v[48:49], v[52:53], v[36:37]
	v_pk_add_f32 v[36:37], v[52:53], v[36:37] neg_lo:[0,1] neg_hi:[0,1]
	s_nop 0
	v_xor_b32_e32 v53, 0x80000000, v36
	v_mov_b32_e32 v52, v37
	v_pk_add_f32 v[36:37], v[46:47], v[48:49]
	v_pk_add_f32 v[46:47], v[46:47], v[48:49] neg_lo:[0,1] neg_hi:[0,1]
	v_pk_add_f32 v[48:49], v[34:35], v[52:53]
	v_pk_add_f32 v[34:35], v[34:35], v[52:53] neg_lo:[0,1] neg_hi:[0,1]
	v_pk_add_f32 v[52:53], v[40:41], v[44:45]
	v_pk_add_f32 v[40:41], v[40:41], v[44:45] neg_lo:[0,1] neg_hi:[0,1]
	v_pk_add_f32 v[44:45], v[26:27], v[38:39]
	v_pk_add_f32 v[26:27], v[26:27], v[38:39] neg_lo:[0,1] neg_hi:[0,1]
	s_nop 0
	v_xor_b32_e32 v39, 0x80000000, v26
	v_mov_b32_e32 v38, v27
	v_pk_add_f32 v[26:27], v[52:53], v[44:45]
	v_pk_add_f32 v[44:45], v[52:53], v[44:45] neg_lo:[0,1] neg_hi:[0,1]
	v_pk_add_f32 v[52:53], v[40:41], v[38:39]
	v_pk_add_f32 v[38:39], v[40:41], v[38:39] neg_lo:[0,1] neg_hi:[0,1]
	v_pk_add_f32 v[40:41], v[18:19], v[42:43]
	v_pk_add_f32 v[18:19], v[18:19], v[42:43] neg_lo:[0,1] neg_hi:[0,1]
	v_pk_add_f32 v[42:43], v[20:21], v[28:29]
	v_pk_add_f32 v[20:21], v[20:21], v[28:29] neg_lo:[0,1] neg_hi:[0,1]
	s_nop 0
	v_xor_b32_e32 v28, 0x80000000, v21
	v_mov_b32_e32 v29, v20
	v_pk_mul_f32 v[28:29], v[50:51], v[28:29] op_sel_hi:[0,1] neg_lo:[1,0] neg_hi:[1,0]
	v_pk_fma_f32 v[20:21], v[50:51], v[20:21], v[28:29] op_sel_hi:[0,1,1]
	v_pk_add_f32 v[28:29], v[22:23], v[30:31]
	v_pk_add_f32 v[22:23], v[22:23], v[30:31] neg_lo:[0,1] neg_hi:[0,1]
	s_nop 0
	v_xor_b32_e32 v31, 0x80000000, v22
	v_mov_b32_e32 v30, v23
	v_pk_add_f32 v[22:23], v[24:25], v[32:33]
	v_pk_add_f32 v[24:25], v[24:25], v[32:33] neg_lo:[0,1] neg_hi:[0,1]
	s_nop 0
	v_xor_b32_e32 v32, 0x80000000, v25
	v_mov_b32_e32 v33, v24
	v_pk_mul_f32 v[32:33], v[50:51], v[32:33] op_sel_hi:[0,1] neg_lo:[1,0] neg_hi:[1,0]
	v_pk_fma_f32 v[24:25], v[50:51], v[24:25], v[32:33] op_sel_hi:[0,1,1] neg_lo:[1,0,0] neg_hi:[1,0,0]
	v_pk_add_f32 v[32:33], v[40:41], v[28:29]
	v_pk_add_f32 v[28:29], v[40:41], v[28:29] neg_lo:[0,1] neg_hi:[0,1]
	v_pk_add_f32 v[40:41], v[42:43], v[22:23]
	v_pk_add_f32 v[22:23], v[42:43], v[22:23] neg_lo:[0,1] neg_hi:[0,1]
	s_nop 0
	v_xor_b32_e32 v43, 0x80000000, v22
	v_mov_b32_e32 v42, v23
	v_pk_add_f32 v[22:23], v[32:33], v[40:41]
	v_pk_add_f32 v[32:33], v[32:33], v[40:41] neg_lo:[0,1] neg_hi:[0,1]
	v_pk_add_f32 v[40:41], v[28:29], v[42:43]
	v_pk_add_f32 v[28:29], v[28:29], v[42:43] neg_lo:[0,1] neg_hi:[0,1]
	v_pk_add_f32 v[42:43], v[18:19], v[30:31]
	v_pk_add_f32 v[18:19], v[18:19], v[30:31] neg_lo:[0,1] neg_hi:[0,1]
	v_pk_add_f32 v[30:31], v[20:21], v[24:25]
	v_pk_add_f32 v[20:21], v[20:21], v[24:25] neg_lo:[0,1] neg_hi:[0,1]
	s_nop 0
	v_xor_b32_e32 v25, 0x80000000, v20
	v_mov_b32_e32 v24, v21
	v_pk_add_f32 v[20:21], v[42:43], v[30:31]
	v_pk_add_f32 v[30:31], v[42:43], v[30:31] neg_lo:[0,1] neg_hi:[0,1]
	v_pk_add_f32 v[42:43], v[18:19], v[24:25]
	v_pk_add_f32 v[18:19], v[18:19], v[24:25] neg_lo:[0,1] neg_hi:[0,1]
	v_add_u32_e32 v24, 0x2000, v14
	v_ashrrev_i32_e32 v25, 31, v24
	v_lshl_add_u64 v[24:25], v[24:25], 3, s[46:47]
	global_store_dwordx2 v[24:25], v[36:37], off
	v_add_u32_e32 v24, 0x2200, v14
	v_ashrrev_i32_e32 v25, 31, v24
	v_lshl_add_u64 v[24:25], v[24:25], 3, s[46:47]
	global_store_dwordx2 v[24:25], v[22:23], off
	v_add_u32_e32 v22, 0x2400, v14
	v_ashrrev_i32_e32 v23, 31, v22
	v_lshl_add_u64 v[22:23], v[22:23], 3, s[46:47]
	global_store_dwordx2 v[22:23], v[26:27], off
	v_add_u32_e32 v22, 0x2600, v14
	v_ashrrev_i32_e32 v23, 31, v22
	v_lshl_add_u64 v[22:23], v[22:23], 3, s[46:47]
	global_store_dwordx2 v[22:23], v[20:21], off
	v_add_u32_e32 v20, 0x2800, v14
	v_ashrrev_i32_e32 v21, 31, v20
	v_lshl_add_u64 v[20:21], v[20:21], 3, s[46:47]
	global_store_dwordx2 v[20:21], v[48:49], off
	v_add_u32_e32 v20, 0x2a00, v14
	v_ashrrev_i32_e32 v21, 31, v20
	v_lshl_add_u64 v[20:21], v[20:21], 3, s[46:47]
	global_store_dwordx2 v[20:21], v[40:41], off
	v_add_u32_e32 v20, 0x2c00, v14
	v_ashrrev_i32_e32 v21, 31, v20
	v_lshl_add_u64 v[20:21], v[20:21], 3, s[46:47]
	global_store_dwordx2 v[20:21], v[52:53], off
	v_add_u32_e32 v20, 0x2e00, v14
	v_ashrrev_i32_e32 v21, 31, v20
	v_lshl_add_u64 v[20:21], v[20:21], 3, s[46:47]
	global_store_dwordx2 v[20:21], v[42:43], off
	v_add_u32_e32 v20, 0x3000, v14
	v_ashrrev_i32_e32 v21, 31, v20
	v_lshl_add_u64 v[20:21], v[20:21], 3, s[46:47]
	global_store_dwordx2 v[20:21], v[46:47], off
	v_add_u32_e32 v20, 0x3200, v14
	v_ashrrev_i32_e32 v21, 31, v20
	v_lshl_add_u64 v[20:21], v[20:21], 3, s[46:47]
	global_store_dwordx2 v[20:21], v[32:33], off
	v_add_u32_e32 v20, 0x3400, v14
	v_ashrrev_i32_e32 v21, 31, v20
	v_lshl_add_u64 v[20:21], v[20:21], 3, s[46:47]
	global_store_dwordx2 v[20:21], v[44:45], off
	v_add_u32_e32 v20, 0x3600, v14
	v_ashrrev_i32_e32 v21, 31, v20
	v_lshl_add_u64 v[20:21], v[20:21], 3, s[46:47]
	global_store_dwordx2 v[20:21], v[30:31], off
	v_add_u32_e32 v20, 0x3800, v14
	v_ashrrev_i32_e32 v21, 31, v20
	v_lshl_add_u64 v[20:21], v[20:21], 3, s[46:47]
	global_store_dwordx2 v[20:21], v[34:35], off
	v_add_u32_e32 v20, 0x3a00, v14
	v_ashrrev_i32_e32 v21, 31, v20
	v_lshl_add_u64 v[20:21], v[20:21], 3, s[46:47]
	global_store_dwordx2 v[20:21], v[28:29], off
	v_add_u32_e32 v20, 0x3c00, v14
	v_add_u32_e32 v14, 0x3e00, v14
	v_ashrrev_i32_e32 v15, 31, v14
	v_ashrrev_i32_e32 v21, 31, v20
	v_lshl_add_u64 v[14:15], v[14:15], 3, s[46:47]
	v_lshl_add_u64 v[20:21], v[20:21], 3, s[46:47]
	global_store_dwordx2 v[14:15], v[18:19], off
	v_mov_b32_e32 v14, v182
	global_store_dwordx2 v[20:21], v[38:39], off
	s_barrier
	v_mov_b32_e32 v40, v169
	v_ashrrev_i32_e32 v15, 31, v14
	v_lshl_add_u64 v[18:19], v[14:15], 2, s[64:65]
	v_add_co_u32_e32 v28, vcc, s0, v18
	s_movk_i32 s0, 0x2000
	s_nop 0
	v_addc_co_u32_e32 v29, vcc, 0, v19, vcc
	v_add_co_u32_e32 v22, vcc, s0, v18
	s_movk_i32 s0, 0x6000
	s_nop 0
	v_addc_co_u32_e32 v23, vcc, 0, v19, vcc
	v_add_co_u32_e32 v30, vcc, s78, v18
	global_load_dword v20, v[18:19], off
	global_load_dword v21, v[18:19], off offset:2048
	v_addc_co_u32_e32 v31, vcc, 0, v19, vcc
	v_add_co_u32_e32 v32, vcc, s43, v18
	v_mov_b32_e32 v15, v173
	s_nop 0
	v_addc_co_u32_e32 v33, vcc, 0, v19, vcc
	v_add_co_u32_e32 v34, vcc, s0, v18
	s_mov_b32 s0, 0x8000
	s_nop 0
	v_addc_co_u32_e32 v35, vcc, 0, v19, vcc
	v_add_co_u32_e32 v36, vcc, s0, v18
	s_mov_b32 s0, 0xa000
	s_nop 0
	v_addc_co_u32_e32 v37, vcc, 0, v19, vcc
	v_add_co_u32_e32 v38, vcc, s0, v18
	global_load_dword v26, v[22:23], off offset:-4096
	global_load_dword v24, v[22:23], off
	global_load_dword v25, v[22:23], off offset:2048
	s_nop 0
	global_load_dword v22, v[32:33], off offset:-4096
	v_addc_co_u32_e32 v39, vcc, 0, v19, vcc
	global_load_dword v43, v[32:33], off offset:2048
	global_load_dword v46, v[34:35], off offset:-4096
	global_load_dword v48, v[36:37], off
	global_load_dword v49, v[36:37], off offset:2048
	global_load_dword v62, v[34:35], off
	global_load_dword v63, v[34:35], off offset:2048
	s_nop 0
	global_load_dword v34, v[38:39], off offset:-4096
	global_load_dword v64, v[36:37], off offset:-4096
	s_mov_b32 s0, 0x9000
	v_add_co_u32_e32 v36, vcc, s0, v18
	s_movk_i32 s0, 0x5000
	s_nop 0
	v_addc_co_u32_e32 v37, vcc, 0, v19, vcc
	global_load_dword v27, v[28:29], off offset:2048
	global_load_dword v35, v[36:37], off offset:2048
	v_add_co_u32_e32 v28, vcc, s0, v18
	s_mov_b32 s0, 0xb000
	s_nop 0
	v_addc_co_u32_e32 v29, vcc, 0, v19, vcc
	global_load_dword v66, v[38:39], off
	global_load_dword v67, v[38:39], off offset:2048
	v_add_co_u32_e32 v36, vcc, s0, v18
	s_mov_b32 s0, 0xc000
	s_nop 0
	v_addc_co_u32_e32 v37, vcc, 0, v19, vcc
	v_add_co_u32_e32 v38, vcc, s0, v18
	s_movk_i32 s0, 0x7000
	s_nop 0
	v_addc_co_u32_e32 v39, vcc, 0, v19, vcc
	global_load_dword v68, v[38:39], off offset:-4096
	global_load_dword v23, v[30:31], off offset:2048
	global_load_dword v69, v[36:37], off offset:2048
	v_add_co_u32_e32 v30, vcc, s0, v18
	s_mov_b32 s0, 0xe000
	s_nop 0
	v_addc_co_u32_e32 v31, vcc, 0, v19, vcc
	global_load_dword v47, v[28:29], off offset:2048
	global_load_dword v65, v[30:31], off offset:2048
	global_load_dword v42, v[32:33], off
	s_nop 0
	global_load_dword v30, v[38:39], off
	global_load_dword v31, v[38:39], off offset:2048
	v_add_co_u32_e32 v28, vcc, s0, v18
	s_mov_b32 s0, 0xd000
	s_nop 0
	v_addc_co_u32_e32 v29, vcc, 0, v19, vcc
	global_load_dword v32, v[28:29], off offset:-4096
	v_add_co_u32_e32 v36, vcc, s0, v18
	s_mov_b32 s0, 0xf000
	s_nop 0
	v_addc_co_u32_e32 v37, vcc, 0, v19, vcc
	global_load_dword v33, v[36:37], off offset:2048
	global_load_dword v38, v[28:29], off
	global_load_dword v39, v[28:29], off offset:2048
	v_add_co_u32_e32 v18, vcc, s0, v18
	v_mov_b32_e32 v36, v165
	s_nop 0
	v_addc_co_u32_e32 v19, vcc, 0, v19, vcc
	global_load_dword v70, v[18:19], off
	global_load_dword v71, v[18:19], off offset:2048
	v_mov_b32_e32 v18, v178
	v_mov_b32_e32 v19, v179
	v_mov_b32_e32 v28, v167
	v_mov_b32_e32 v45, v11
	v_mov_b32_e32 v10, v171
	s_waitcnt vmcnt(22)
	v_sub_f32_e32 v44, v21, v49
	v_mov_b32_e32 v13, v44
	v_pk_mul_f32 v[50:51], v[12:13], v[78:79] op_sel_hi:[1,0] neg_lo:[0,1] neg_hi:[0,1]
	v_sub_f32_e32 v10, v20, v48
	v_pk_fma_f32 v[44:45], v[44:45], v[72:73], v[50:51] op_sel_hi:[1,0,1]
	s_waitcnt vmcnt(19)
	v_sub_f32_e32 v50, v26, v34
	v_mov_b32_e32 v13, v50
	v_mov_b32_e32 v51, v11
	v_pk_mul_f32 v[52:53], v[12:13], v[40:41] op_sel_hi:[1,0] neg_lo:[0,1] neg_hi:[0,1]
	v_pk_add_f32 v[20:21], v[20:21], v[48:49]
	v_pk_fma_f32 v[50:51], v[50:51], v[36:37], v[52:53] op_sel_hi:[1,0,1]
	s_waitcnt vmcnt(16)
	v_sub_f32_e32 v52, v27, v35
	v_mov_b32_e32 v13, v52
	v_mov_b32_e32 v53, v11
	v_pk_mul_f32 v[54:55], v[12:13], v[76:77] op_sel_hi:[1,0] neg_lo:[0,1] neg_hi:[0,1]
	v_pk_add_f32 v[26:27], v[26:27], v[34:35]
	v_pk_fma_f32 v[54:55], v[52:53], v[74:75], v[54:55] op_sel_hi:[1,0,1]
	s_waitcnt vmcnt(15)
	v_sub_f32_e32 v52, v24, v66
	v_mov_b32_e32 v13, v52
	v_pk_mul_f32 v[56:57], v[12:13], v[28:29] op_sel_hi:[1,0] neg_lo:[0,1] neg_hi:[0,1]
	s_waitcnt vmcnt(6)
	v_sub_f32_e32 v82, v43, v31
	v_pk_fma_f32 v[56:57], v[52:53], v[28:29], v[56:57] op_sel_hi:[1,0,1]
	v_sub_f32_e32 v52, v25, v67
	v_pk_mul_f32 v[58:59], v[52:53], v[76:77] op_sel_hi:[1,0]
	v_mov_b32_e32 v13, v52
	v_sub_f32_e32 v52, v22, v68
	v_pk_fma_f32 v[60:61], v[12:13], v[74:75], v[58:59] op_sel_hi:[1,0,1] neg_lo:[0,1,0] neg_hi:[0,1,0]
	v_pk_mul_f32 v[58:59], v[52:53], v[40:41] op_sel_hi:[1,0]
	v_mov_b32_e32 v13, v52
	v_sub_f32_e32 v52, v23, v69
	v_pk_fma_f32 v[58:59], v[12:13], v[36:37], v[58:59] op_sel_hi:[1,0,1] neg_lo:[0,1,0] neg_hi:[0,1,0]
	v_pk_mul_f32 v[80:81], v[52:53], v[78:79] op_sel_hi:[1,0]
	v_mov_b32_e32 v13, v52
	v_pk_fma_f32 v[52:53], v[12:13], v[72:73], v[80:81] op_sel_hi:[1,0,1] neg_lo:[0,1,0] neg_hi:[0,1,0]
	v_sub_f32_e32 v13, v42, v30
	v_xor_b32_e32 v81, 0x80000000, v13
	v_pk_mul_f32 v[84:85], v[82:83], v[78:79] op_sel_hi:[1,0] neg_lo:[0,1] neg_hi:[0,1]
	v_mov_b32_e32 v13, v82
	v_pk_fma_f32 v[82:83], v[12:13], v[72:73], v[84:85] op_sel_hi:[1,0,1] neg_lo:[0,1,0] neg_hi:[0,1,0]
	s_waitcnt vmcnt(5)
	v_sub_f32_e32 v84, v46, v32
	v_mov_b32_e32 v85, v11
	v_pk_mul_f32 v[86:87], v[84:85], v[40:41] op_sel_hi:[1,0] neg_lo:[0,1] neg_hi:[0,1]
	v_mov_b32_e32 v13, v84
	v_pk_fma_f32 v[84:85], v[12:13], v[36:37], v[86:87] op_sel_hi:[1,0,1] neg_lo:[0,1,0] neg_hi:[0,1,0]
	s_waitcnt vmcnt(4)
	v_sub_f32_e32 v86, v47, v33
	v_mov_b32_e32 v87, v11
	v_pk_mul_f32 v[88:89], v[86:87], v[76:77] op_sel_hi:[1,0] neg_lo:[0,1] neg_hi:[0,1]
	v_mov_b32_e32 v13, v86
	v_pk_fma_f32 v[86:87], v[12:13], v[74:75], v[88:89] op_sel_hi:[1,0,1] neg_lo:[0,1,0] neg_hi:[0,1,0]
	s_waitcnt vmcnt(3)
	v_sub_f32_e32 v88, v62, v38
	v_mov_b32_e32 v13, v88
	v_mov_b32_e32 v89, v11
	v_pk_mul_f32 v[90:91], v[12:13], v[28:29] op_sel_hi:[1,0] neg_lo:[0,1] neg_hi:[0,1]
	v_pk_add_f32 v[30:31], v[42:43], v[30:31]
	v_pk_fma_f32 v[88:89], v[88:89], v[28:29], v[90:91] op_sel_hi:[1,0,1] neg_lo:[0,1,0] neg_hi:[0,1,0]
	s_waitcnt vmcnt(2)
	v_sub_f32_e32 v90, v63, v39
	v_mov_b32_e32 v13, v90
	v_mov_b32_e32 v91, v11
	v_pk_mul_f32 v[76:77], v[12:13], v[76:77] op_sel_hi:[1,0] neg_lo:[0,1] neg_hi:[0,1]
	v_pk_add_f32 v[42:43], v[20:21], v[30:31] neg_lo:[0,1] neg_hi:[0,1]
	v_pk_fma_f32 v[74:75], v[90:91], v[74:75], v[76:77] op_sel_hi:[1,0,1] neg_lo:[0,1,0] neg_hi:[0,1,0]
	s_waitcnt vmcnt(1)
	v_sub_f32_e32 v76, v64, v70
	v_mov_b32_e32 v13, v76
	v_mov_b32_e32 v77, v11
	v_pk_mul_f32 v[90:91], v[12:13], v[40:41] op_sel_hi:[1,0] neg_lo:[0,1] neg_hi:[0,1]
	v_pk_add_f32 v[32:33], v[46:47], v[32:33]
	v_pk_fma_f32 v[76:77], v[76:77], v[36:37], v[90:91] op_sel_hi:[1,0,1] neg_lo:[0,1,0] neg_hi:[0,1,0]
	s_waitcnt vmcnt(0)
	v_sub_f32_e32 v90, v65, v71
	v_mov_b32_e32 v13, v90
	v_pk_mul_f32 v[78:79], v[12:13], v[78:79] op_sel_hi:[1,0] neg_lo:[0,1] neg_hi:[0,1]
	v_mov_b32_e32 v13, v43
	v_mov_b32_e32 v46, v42
	v_pk_add_f32 v[20:21], v[20:21], v[30:31]
	v_mov_b32_e32 v30, v43
	v_mov_b32_e32 v31, v11
	v_pk_mul_f32 v[42:43], v[12:13], v[40:41] op_sel_hi:[1,0] neg_lo:[0,1] neg_hi:[0,1]
	v_pk_add_f32 v[34:35], v[62:63], v[38:39]
	v_pk_fma_f32 v[62:63], v[30:31], v[36:37], v[42:43] op_sel_hi:[1,0,1]
	v_pk_add_f32 v[30:31], v[26:27], v[32:33] neg_lo:[0,1] neg_hi:[0,1]
	v_pk_add_f32 v[24:25], v[24:25], v[66:67]
	v_mov_b32_e32 v13, v30
	v_mov_b32_e32 v42, v30
	v_pk_mul_f32 v[48:49], v[12:13], v[28:29] op_sel_hi:[1,0] neg_lo:[0,1] neg_hi:[0,1]
	v_pk_add_f32 v[26:27], v[26:27], v[32:33]
	v_mov_b32_e32 v32, v31
	v_mov_b32_e32 v33, v11
	v_mov_b32_e32 v13, v31
	v_pk_add_f32 v[30:31], v[24:25], v[34:35] neg_lo:[0,1] neg_hi:[0,1]
	v_pk_add_f32 v[22:23], v[22:23], v[68:69]
	v_pk_add_f32 v[38:39], v[64:65], v[70:71]
	v_pk_mul_f32 v[32:33], v[32:33], v[40:41] op_sel_hi:[1,0]
	v_pk_add_f32 v[24:25], v[24:25], v[34:35]
	v_mov_b32_e32 v34, v31
	v_mov_b32_e32 v35, v11
	v_pk_fma_f32 v[32:33], v[12:13], v[36:37], v[32:33] op_sel_hi:[1,0,1] neg_lo:[0,1,0] neg_hi:[0,1,0]
	v_xor_b32_e32 v67, 0x80000000, v30
	v_pk_mul_f32 v[34:35], v[34:35], v[40:41] op_sel_hi:[1,0] neg_lo:[0,1] neg_hi:[0,1]
	v_mov_b32_e32 v13, v31
	v_pk_add_f32 v[30:31], v[22:23], v[38:39] neg_lo:[0,1] neg_hi:[0,1]
	v_mov_b32_e32 v43, v11
	v_pk_fma_f32 v[68:69], v[12:13], v[36:37], v[34:35] op_sel_hi:[1,0,1] neg_lo:[0,1,0] neg_hi:[0,1,0]
	v_mov_b32_e32 v13, v30
	v_pk_fma_f32 v[64:65], v[42:43], v[28:29], v[48:49] op_sel_hi:[1,0,1]
	v_mov_b32_e32 v34, v30
	v_mov_b32_e32 v35, v11
	v_pk_mul_f32 v[42:43], v[12:13], v[28:29] op_sel_hi:[1,0] neg_lo:[0,1] neg_hi:[0,1]
	v_mov_b32_e32 v13, v31
	v_pk_fma_f32 v[70:71], v[34:35], v[28:29], v[42:43] op_sel_hi:[1,0,1] neg_lo:[0,1,0] neg_hi:[0,1,0]
	v_mov_b32_e32 v34, v31
	v_pk_mul_f32 v[30:31], v[12:13], v[40:41] op_sel_hi:[1,0] neg_lo:[0,1] neg_hi:[0,1]
	v_pk_add_f32 v[22:23], v[22:23], v[38:39]
	v_pk_fma_f32 v[38:39], v[34:35], v[36:37], v[30:31] op_sel_hi:[1,0,1] neg_lo:[0,1,0] neg_hi:[0,1,0]
	v_pk_add_f32 v[30:31], v[20:21], v[24:25] neg_lo:[0,1] neg_hi:[0,1]
	v_pk_add_f32 v[20:21], v[20:21], v[24:25]
	v_mov_b32_e32 v13, v31
	v_mov_b32_e32 v42, v30
	v_mov_b32_e32 v24, v31
	v_mov_b32_e32 v25, v11
	v_pk_mul_f32 v[30:31], v[12:13], v[28:29] op_sel_hi:[1,0] neg_lo:[0,1] neg_hi:[0,1]
	v_mov_b32_e32 v91, v11
	v_pk_fma_f32 v[30:31], v[24:25], v[28:29], v[30:31] op_sel_hi:[1,0,1]
	v_pk_add_f32 v[24:25], v[26:27], v[22:23] neg_lo:[0,1] neg_hi:[0,1]
	v_pk_fma_f32 v[72:73], v[90:91], v[72:73], v[78:79] op_sel_hi:[1,0,1] neg_lo:[0,1,0] neg_hi:[0,1,0]
	v_mov_b32_e32 v13, v25
	v_xor_b32_e32 v79, 0x80000000, v24
	v_pk_add_f32 v[22:23], v[26:27], v[22:23]
	v_mov_b32_e32 v26, v25
	v_mov_b32_e32 v27, v11
	v_pk_mul_f32 v[24:25], v[12:13], v[28:29] op_sel_hi:[1,0] neg_lo:[0,1] neg_hi:[0,1]
	v_pk_add_f32 v[34:35], v[20:21], v[22:23]
	v_pk_fma_f32 v[26:27], v[26:27], v[28:29], v[24:25] op_sel_hi:[1,0,1] neg_lo:[0,1,0] neg_hi:[0,1,0]
	v_pk_add_f32 v[24:25], v[20:21], v[22:23] neg_lo:[0,1] neg_hi:[0,1]
	v_mov_b32_e32 v43, v11
	v_pk_add_f32 v[20:21], v[24:25], 0 neg_lo:[1,1] neg_hi:[1,1]
	v_mov_b32_e32 v78, v11
	v_mov_b32_e32 v90, v24
	v_mov_b32_e32 v20, v11
	v_pk_add_f32 v[48:49], v[90:91], v[20:21]
	v_pk_add_f32 v[24:25], v[90:91], v[20:21] neg_lo:[0,1] neg_hi:[0,1]
	v_pk_add_f32 v[20:21], v[42:43], v[78:79]
	v_pk_add_f32 v[22:23], v[42:43], v[78:79] neg_lo:[0,1] neg_hi:[0,1]
	v_pk_add_f32 v[42:43], v[30:31], v[26:27]
	v_pk_add_f32 v[26:27], v[30:31], v[26:27] neg_lo:[0,1] neg_hi:[0,1]
	v_mov_b32_e32 v47, v11
	v_mov_b32_e32 v66, v11
	v_xor_b32_e32 v79, 0x80000000, v26
	v_mov_b32_e32 v78, v27
	v_pk_add_f32 v[26:27], v[62:63], v[68:69]
	v_pk_add_f32 v[62:63], v[62:63], v[68:69] neg_lo:[0,1] neg_hi:[0,1]
	v_pk_add_f32 v[90:91], v[20:21], v[42:43]
	v_pk_add_f32 v[30:31], v[20:21], v[42:43] neg_lo:[0,1] neg_hi:[0,1]
	v_pk_add_f32 v[42:43], v[22:23], v[78:79]
	v_pk_add_f32 v[20:21], v[22:23], v[78:79] neg_lo:[0,1] neg_hi:[0,1]
	v_pk_add_f32 v[22:23], v[46:47], v[66:67]
	v_pk_add_f32 v[46:47], v[46:47], v[66:67] neg_lo:[0,1] neg_hi:[0,1]
	v_xor_b32_e32 v66, 0x80000000, v63
	v_mov_b32_e32 v67, v62
	v_pk_mul_f32 v[66:67], v[28:29], v[66:67] op_sel_hi:[0,1] neg_lo:[1,0] neg_hi:[1,0]
	v_pk_fma_f32 v[66:67], v[28:29], v[62:63], v[66:67] op_sel_hi:[0,1,1]
	v_pk_add_f32 v[62:63], v[64:65], v[70:71]
	v_pk_add_f32 v[64:65], v[64:65], v[70:71] neg_lo:[0,1] neg_hi:[0,1]
	v_mov_b32_e32 v80, v11
	v_xor_b32_e32 v69, 0x80000000, v64
	v_mov_b32_e32 v68, v65
	v_pk_add_f32 v[64:65], v[32:33], v[38:39]
	v_pk_add_f32 v[32:33], v[32:33], v[38:39] neg_lo:[0,1] neg_hi:[0,1]
	v_pk_add_f32 v[78:79], v[44:45], v[82:83]
	v_xor_b32_e32 v38, 0x80000000, v33
	v_mov_b32_e32 v39, v32
	v_pk_mul_f32 v[38:39], v[28:29], v[38:39] op_sel_hi:[0,1] neg_lo:[1,0] neg_hi:[1,0]
	v_pk_fma_f32 v[32:33], v[28:29], v[32:33], v[38:39] op_sel_hi:[0,1,1] neg_lo:[1,0,0] neg_hi:[1,0,0]
	v_pk_add_f32 v[38:39], v[22:23], v[62:63]
	v_pk_add_f32 v[22:23], v[22:23], v[62:63] neg_lo:[0,1] neg_hi:[0,1]
	v_pk_add_f32 v[62:63], v[26:27], v[64:65]
	v_pk_add_f32 v[26:27], v[26:27], v[64:65] neg_lo:[0,1] neg_hi:[0,1]
	v_pk_add_f32 v[70:71], v[38:39], v[62:63]
	v_xor_b32_e32 v65, 0x80000000, v26
	v_mov_b32_e32 v64, v27
	v_pk_add_f32 v[38:39], v[38:39], v[62:63] neg_lo:[0,1] neg_hi:[0,1]
	v_pk_add_f32 v[62:63], v[22:23], v[64:65]
	v_pk_add_f32 v[26:27], v[22:23], v[64:65] neg_lo:[0,1] neg_hi:[0,1]
	v_pk_add_f32 v[22:23], v[46:47], v[68:69]
	v_pk_add_f32 v[64:65], v[46:47], v[68:69] neg_lo:[0,1] neg_hi:[0,1]
	v_pk_add_f32 v[46:47], v[66:67], v[32:33]
	v_pk_add_f32 v[32:33], v[66:67], v[32:33] neg_lo:[0,1] neg_hi:[0,1]
	v_pk_add_f32 v[44:45], v[44:45], v[82:83] neg_lo:[0,1] neg_hi:[0,1]
	v_xor_b32_e32 v67, 0x80000000, v32
	v_mov_b32_e32 v66, v33
	v_pk_add_f32 v[68:69], v[22:23], v[46:47]
	v_pk_add_f32 v[32:33], v[22:23], v[46:47] neg_lo:[0,1] neg_hi:[0,1]
	v_pk_add_f32 v[46:47], v[64:65], v[66:67]
	v_pk_add_f32 v[22:23], v[64:65], v[66:67] neg_lo:[0,1] neg_hi:[0,1]
	v_pk_add_f32 v[64:65], v[10:11], v[80:81]
	v_pk_add_f32 v[66:67], v[10:11], v[80:81] neg_lo:[0,1] neg_hi:[0,1]
	v_xor_b32_e32 v80, 0x80000000, v45
	v_mov_b32_e32 v81, v44
	v_pk_mul_f32 v[80:81], v[40:41], v[80:81] op_sel_hi:[0,1] neg_lo:[1,0] neg_hi:[1,0]
	v_pk_fma_f32 v[44:45], v[36:37], v[44:45], v[80:81] op_sel_hi:[0,1,1]
	v_pk_add_f32 v[80:81], v[50:51], v[84:85]
	v_pk_add_f32 v[50:51], v[50:51], v[84:85] neg_lo:[0,1] neg_hi:[0,1]
	v_add_f32_e32 v10, v34, v35
	v_xor_b32_e32 v82, 0x80000000, v51
	v_mov_b32_e32 v83, v50
	v_pk_mul_f32 v[82:83], v[28:29], v[82:83] op_sel_hi:[0,1] neg_lo:[1,0] neg_hi:[1,0]
	v_pk_fma_f32 v[82:83], v[28:29], v[50:51], v[82:83] op_sel_hi:[0,1,1]
	v_pk_add_f32 v[50:51], v[54:55], v[86:87]
	v_pk_add_f32 v[54:55], v[54:55], v[86:87] neg_lo:[0,1] neg_hi:[0,1]
	v_pk_fma_f32 v[16:17], v[10:11], s[94:95], v[16:17] op_sel_hi:[0,1,1]
	v_xor_b32_e32 v84, 0x80000000, v55
	v_mov_b32_e32 v85, v54
	v_pk_mul_f32 v[84:85], v[36:37], v[84:85] op_sel_hi:[0,1] neg_lo:[1,0] neg_hi:[1,0]
	v_pk_fma_f32 v[84:85], v[40:41], v[54:55], v[84:85] op_sel_hi:[0,1,1]
	v_pk_add_f32 v[54:55], v[56:57], v[88:89]
	v_pk_add_f32 v[56:57], v[56:57], v[88:89] neg_lo:[0,1] neg_hi:[0,1]
	v_lshl_add_u32 v13, v15, 3, 0
	v_xor_b32_e32 v87, 0x80000000, v56
	v_mov_b32_e32 v86, v57
	v_pk_add_f32 v[56:57], v[60:61], v[74:75]
	v_pk_add_f32 v[60:61], v[60:61], v[74:75] neg_lo:[0,1] neg_hi:[0,1]
	ds_write_b64 v13, v[16:17]
	v_xor_b32_e32 v74, 0x80000000, v61
	v_mov_b32_e32 v75, v60
	v_pk_mul_f32 v[74:75], v[36:37], v[74:75] op_sel_hi:[0,1] neg_lo:[1,0] neg_hi:[1,0]
	v_pk_fma_f32 v[60:61], v[40:41], v[60:61], v[74:75] op_sel_hi:[0,1,1] neg_lo:[1,0,0] neg_hi:[1,0,0]
	v_pk_add_f32 v[74:75], v[58:59], v[76:77]
	v_pk_add_f32 v[58:59], v[58:59], v[76:77] neg_lo:[0,1] neg_hi:[0,1]
	v_pk_fma_f32 v[16:17], v[18:19], s[90:91], v[18:19] op_sel:[1,0,0] op_sel_hi:[0,1,1]
	v_xor_b32_e32 v76, 0x80000000, v59
	v_mov_b32_e32 v77, v58
	v_pk_mul_f32 v[76:77], v[28:29], v[76:77] op_sel_hi:[0,1] neg_lo:[1,0] neg_hi:[1,0]
	v_pk_fma_f32 v[58:59], v[28:29], v[58:59], v[76:77] op_sel_hi:[0,1,1] neg_lo:[1,0,0] neg_hi:[1,0,0]
	v_pk_add_f32 v[76:77], v[52:53], v[72:73]
	v_pk_add_f32 v[52:53], v[52:53], v[72:73] neg_lo:[0,1] neg_hi:[0,1]
	s_nop 0
	v_xor_b32_e32 v72, 0x80000000, v53
	v_mov_b32_e32 v73, v52
	v_pk_mul_f32 v[40:41], v[40:41], v[72:73] op_sel_hi:[0,1] neg_lo:[1,0] neg_hi:[1,0]
	v_pk_fma_f32 v[52:53], v[36:37], v[52:53], v[40:41] op_sel_hi:[0,1,1] neg_lo:[1,0,0] neg_hi:[1,0,0]
	v_pk_add_f32 v[36:37], v[64:65], v[54:55]
	v_pk_add_f32 v[64:65], v[64:65], v[54:55] neg_lo:[0,1] neg_hi:[0,1]
	v_pk_add_f32 v[54:55], v[78:79], v[56:57] neg_lo:[0,1] neg_hi:[0,1]
	v_pk_add_f32 v[40:41], v[56:57], v[78:79]
	v_xor_b32_e32 v56, 0x80000000, v55
	v_mov_b32_e32 v57, v54
	v_pk_mul_f32 v[56:57], v[28:29], v[56:57] op_sel_hi:[0,1] neg_lo:[1,0] neg_hi:[1,0]
	v_pk_add_f32 v[72:73], v[80:81], v[74:75] neg_lo:[0,1] neg_hi:[0,1]
	v_pk_fma_f32 v[56:57], v[28:29], v[54:55], v[56:57] op_sel_hi:[0,1,1]
	v_pk_add_f32 v[54:55], v[80:81], v[74:75]
	v_xor_b32_e32 v75, 0x80000000, v72
	v_mov_b32_e32 v74, v73
	v_pk_add_f32 v[72:73], v[50:51], v[76:77]
	v_pk_add_f32 v[50:51], v[50:51], v[76:77] neg_lo:[0,1] neg_hi:[0,1]
	s_nop 0
	v_xor_b32_e32 v76, 0x80000000, v51
	v_mov_b32_e32 v77, v50
	v_pk_mul_f32 v[76:77], v[28:29], v[76:77] op_sel_hi:[0,1] neg_lo:[1,0] neg_hi:[1,0]
	v_pk_fma_f32 v[50:51], v[28:29], v[50:51], v[76:77] op_sel_hi:[0,1,1] neg_lo:[1,0,0] neg_hi:[1,0,0]
	v_pk_add_f32 v[76:77], v[36:37], v[54:55]
	v_pk_add_f32 v[36:37], v[36:37], v[54:55] neg_lo:[0,1] neg_hi:[0,1]
	v_pk_add_f32 v[54:55], v[40:41], v[72:73]
	v_pk_add_f32 v[40:41], v[40:41], v[72:73] neg_lo:[0,1] neg_hi:[0,1]
	v_pk_add_f32 v[78:79], v[76:77], v[54:55]
	v_xor_b32_e32 v73, 0x80000000, v40
	v_mov_b32_e32 v72, v41
	v_pk_add_f32 v[54:55], v[76:77], v[54:55] neg_lo:[0,1] neg_hi:[0,1]
	v_pk_add_f32 v[76:77], v[36:37], v[72:73]
	v_pk_add_f32 v[40:41], v[36:37], v[72:73] neg_lo:[0,1] neg_hi:[0,1]
	v_pk_add_f32 v[72:73], v[56:57], v[50:51]
	v_pk_add_f32 v[50:51], v[56:57], v[50:51] neg_lo:[0,1] neg_hi:[0,1]
	v_pk_add_f32 v[36:37], v[64:65], v[74:75]
	v_pk_add_f32 v[64:65], v[64:65], v[74:75] neg_lo:[0,1] neg_hi:[0,1]
	v_xor_b32_e32 v57, 0x80000000, v50
	v_mov_b32_e32 v56, v51
	v_pk_add_f32 v[74:75], v[36:37], v[72:73]
	v_pk_add_f32 v[50:51], v[36:37], v[72:73] neg_lo:[0,1] neg_hi:[0,1]
	v_pk_add_f32 v[72:73], v[64:65], v[56:57]
	v_pk_add_f32 v[36:37], v[64:65], v[56:57] neg_lo:[0,1] neg_hi:[0,1]
	v_pk_add_f32 v[56:57], v[66:67], v[86:87]
	v_pk_add_f32 v[64:65], v[66:67], v[86:87] neg_lo:[0,1] neg_hi:[0,1]
	v_pk_add_f32 v[66:67], v[60:61], v[44:45]
	v_pk_add_f32 v[44:45], v[44:45], v[60:61] neg_lo:[0,1] neg_hi:[0,1]
	s_nop 0
	v_xor_b32_e32 v60, 0x80000000, v45
	v_mov_b32_e32 v61, v44
	v_pk_mul_f32 v[60:61], v[28:29], v[60:61] op_sel_hi:[0,1] neg_lo:[1,0] neg_hi:[1,0]
	v_pk_fma_f32 v[60:61], v[28:29], v[44:45], v[60:61] op_sel_hi:[0,1,1]
	v_pk_add_f32 v[44:45], v[82:83], v[58:59]
	v_pk_add_f32 v[58:59], v[82:83], v[58:59] neg_lo:[0,1] neg_hi:[0,1]
	s_nop 0
	v_xor_b32_e32 v81, 0x80000000, v58
	v_mov_b32_e32 v80, v59
	v_pk_add_f32 v[58:59], v[84:85], v[52:53]
	v_pk_add_f32 v[52:53], v[84:85], v[52:53] neg_lo:[0,1] neg_hi:[0,1]
	s_nop 0
	v_xor_b32_e32 v82, 0x80000000, v53
	v_mov_b32_e32 v83, v52
	v_pk_mul_f32 v[82:83], v[28:29], v[82:83] op_sel_hi:[0,1] neg_lo:[1,0] neg_hi:[1,0]
	v_pk_fma_f32 v[28:29], v[28:29], v[52:53], v[82:83] op_sel_hi:[0,1,1] neg_lo:[1,0,0] neg_hi:[1,0,0]
	v_pk_add_f32 v[52:53], v[56:57], v[44:45]
	v_pk_add_f32 v[44:45], v[56:57], v[44:45] neg_lo:[0,1] neg_hi:[0,1]
	v_pk_add_f32 v[56:57], v[66:67], v[58:59]
	v_pk_add_f32 v[58:59], v[66:67], v[58:59] neg_lo:[0,1] neg_hi:[0,1]
	s_nop 0
	v_xor_b32_e32 v67, 0x80000000, v58
	v_mov_b32_e32 v66, v59
	v_pk_add_f32 v[82:83], v[44:45], v[66:67]
	v_pk_add_f32 v[44:45], v[44:45], v[66:67] neg_lo:[0,1] neg_hi:[0,1]
	v_pk_add_f32 v[66:67], v[60:61], v[28:29]
	v_pk_add_f32 v[28:29], v[60:61], v[28:29] neg_lo:[0,1] neg_hi:[0,1]
	v_pk_add_f32 v[58:59], v[52:53], v[56:57]
	v_pk_add_f32 v[56:57], v[52:53], v[56:57] neg_lo:[0,1] neg_hi:[0,1]
	v_pk_add_f32 v[52:53], v[64:65], v[80:81]
	v_pk_add_f32 v[64:65], v[64:65], v[80:81] neg_lo:[0,1] neg_hi:[0,1]
	v_xor_b32_e32 v61, 0x80000000, v28
	v_mov_b32_e32 v60, v29
	v_pk_add_f32 v[80:81], v[52:53], v[66:67]
	v_pk_add_f32 v[52:53], v[52:53], v[66:67] neg_lo:[0,1] neg_hi:[0,1]
	v_pk_add_f32 v[66:67], v[64:65], v[60:61]
	v_pk_add_f32 v[28:29], v[64:65], v[60:61] neg_lo:[0,1] neg_hi:[0,1]
	v_xor_b32_e32 v60, 0x80000000, v79
	v_mov_b32_e32 v61, v79
	v_pk_mul_f32 v[60:61], v[16:17], v[60:61] op_sel:[1,0] op_sel_hi:[0,1]
	v_pk_fma_f32 v[60:61], v[16:17], v[78:79], v[60:61] op_sel_hi:[1,0,1]
	ds_write_b64 v13, v[60:61] offset:4224
	v_xor_b32_e32 v60, 0x80000000, v17
	v_mov_b32_e32 v61, v17
	v_pk_mul_f32 v[60:61], v[18:19], v[60:61] op_sel:[1,0] op_sel_hi:[0,1]
	v_pk_fma_f32 v[16:17], v[18:19], v[16:17], v[60:61] op_sel_hi:[1,0,1]
	v_xor_b32_e32 v60, 0x80000000, v71
	v_mov_b32_e32 v61, v71
	v_pk_mul_f32 v[60:61], v[16:17], v[60:61] op_sel:[1,0] op_sel_hi:[0,1]
	v_pk_fma_f32 v[60:61], v[16:17], v[70:71], v[60:61] op_sel_hi:[1,0,1]
	ds_write_b64 v13, v[60:61] offset:8448
	v_xor_b32_e32 v60, 0x80000000, v17
	v_mov_b32_e32 v61, v17
	v_pk_mul_f32 v[60:61], v[18:19], v[60:61] op_sel:[1,0] op_sel_hi:[0,1]
	v_pk_fma_f32 v[16:17], v[18:19], v[16:17], v[60:61] op_sel_hi:[1,0,1]
	v_xor_b32_e32 v60, 0x80000000, v59
	v_mov_b32_e32 v61, v59
	v_pk_mul_f32 v[60:61], v[16:17], v[60:61] op_sel:[1,0] op_sel_hi:[0,1]
	v_pk_fma_f32 v[58:59], v[16:17], v[58:59], v[60:61] op_sel_hi:[1,0,1]
	ds_write_b64 v13, v[58:59] offset:12672
	v_xor_b32_e32 v58, 0x80000000, v17
	v_mov_b32_e32 v59, v17
	v_pk_mul_f32 v[58:59], v[18:19], v[58:59] op_sel:[1,0] op_sel_hi:[0,1]
	v_pk_fma_f32 v[16:17], v[18:19], v[16:17], v[58:59] op_sel_hi:[1,0,1]
	v_xor_b32_e32 v58, 0x80000000, v91
	v_mov_b32_e32 v59, v91
	v_pk_mul_f32 v[58:59], v[58:59], v[16:17] op_sel:[0,1] op_sel_hi:[1,0]
	s_nop 0
	v_pk_fma_f32 v[58:59], v[90:91], v[16:17], v[58:59] op_sel_hi:[0,1,1]
	ds_write_b64 v13, v[58:59] offset:16896
	v_xor_b32_e32 v58, 0x80000000, v17
	v_mov_b32_e32 v59, v17
	v_pk_mul_f32 v[58:59], v[18:19], v[58:59] op_sel:[1,0] op_sel_hi:[0,1]
	v_pk_fma_f32 v[16:17], v[18:19], v[16:17], v[58:59] op_sel_hi:[1,0,1]
	v_xor_b32_e32 v58, 0x80000000, v75
	v_mov_b32_e32 v59, v75
	v_pk_mul_f32 v[58:59], v[16:17], v[58:59] op_sel:[1,0] op_sel_hi:[0,1]
	v_pk_fma_f32 v[58:59], v[16:17], v[74:75], v[58:59] op_sel_hi:[1,0,1]
	ds_write_b64 v13, v[58:59] offset:21120
	v_xor_b32_e32 v58, 0x80000000, v17
	v_mov_b32_e32 v59, v17
	v_pk_mul_f32 v[58:59], v[18:19], v[58:59] op_sel:[1,0] op_sel_hi:[0,1]
	v_pk_fma_f32 v[16:17], v[18:19], v[16:17], v[58:59] op_sel_hi:[1,0,1]
	v_xor_b32_e32 v58, 0x80000000, v69
	v_mov_b32_e32 v59, v69
	v_pk_mul_f32 v[58:59], v[58:59], v[16:17] op_sel:[0,1] op_sel_hi:[1,0]
	s_nop 0
	v_pk_fma_f32 v[58:59], v[68:69], v[16:17], v[58:59] op_sel_hi:[0,1,1]
	ds_write_b64 v13, v[58:59] offset:25344
	v_xor_b32_e32 v58, 0x80000000, v17
	v_mov_b32_e32 v59, v17
	v_pk_mul_f32 v[58:59], v[18:19], v[58:59] op_sel:[1,0] op_sel_hi:[0,1]
	v_pk_fma_f32 v[16:17], v[18:19], v[16:17], v[58:59] op_sel_hi:[1,0,1]
	v_xor_b32_e32 v58, 0x80000000, v81
	v_mov_b32_e32 v59, v81
	v_pk_mul_f32 v[58:59], v[58:59], v[16:17] op_sel:[0,1] op_sel_hi:[1,0]
	s_nop 0
	v_pk_fma_f32 v[58:59], v[80:81], v[16:17], v[58:59] op_sel_hi:[0,1,1]
	ds_write_b64 v13, v[58:59] offset:29568
	v_xor_b32_e32 v58, 0x80000000, v17
	v_mov_b32_e32 v59, v17
	v_pk_mul_f32 v[58:59], v[18:19], v[58:59] op_sel:[1,0] op_sel_hi:[0,1]
	v_pk_fma_f32 v[16:17], v[18:19], v[16:17], v[58:59] op_sel_hi:[1,0,1]
	v_xor_b32_e32 v58, 0x80000000, v49
	v_mov_b32_e32 v59, v49
	v_pk_mul_f32 v[58:59], v[58:59], v[16:17] op_sel:[0,1] op_sel_hi:[1,0]
	s_nop 0
	v_pk_fma_f32 v[48:49], v[48:49], v[16:17], v[58:59] op_sel_hi:[0,1,1]
	ds_write_b64 v13, v[48:49] offset:33792
	v_xor_b32_e32 v48, 0x80000000, v17
	v_mov_b32_e32 v49, v17
	v_pk_mul_f32 v[48:49], v[18:19], v[48:49] op_sel:[1,0] op_sel_hi:[0,1]
	v_pk_fma_f32 v[16:17], v[18:19], v[16:17], v[48:49] op_sel_hi:[1,0,1]
	v_xor_b32_e32 v48, 0x80000000, v77
	v_mov_b32_e32 v49, v77
	v_pk_mul_f32 v[48:49], v[48:49], v[16:17] op_sel:[0,1] op_sel_hi:[1,0]
	s_nop 0
	v_pk_fma_f32 v[48:49], v[76:77], v[16:17], v[48:49] op_sel_hi:[0,1,1]
	ds_write_b64 v13, v[48:49] offset:38016
	v_xor_b32_e32 v48, 0x80000000, v17
	v_mov_b32_e32 v49, v17
	v_pk_mul_f32 v[48:49], v[18:19], v[48:49] op_sel:[1,0] op_sel_hi:[0,1]
	v_pk_fma_f32 v[16:17], v[18:19], v[16:17], v[48:49] op_sel_hi:[1,0,1]
	v_xor_b32_e32 v48, 0x80000000, v63
	v_mov_b32_e32 v49, v63
	v_pk_mul_f32 v[48:49], v[48:49], v[16:17] op_sel:[0,1] op_sel_hi:[1,0]
	s_nop 0
	v_pk_fma_f32 v[48:49], v[62:63], v[16:17], v[48:49] op_sel_hi:[0,1,1]
	ds_write_b64 v13, v[48:49] offset:42240
	v_xor_b32_e32 v48, 0x80000000, v17
	v_mov_b32_e32 v49, v17
	v_pk_mul_f32 v[48:49], v[18:19], v[48:49] op_sel:[1,0] op_sel_hi:[0,1]
	v_pk_fma_f32 v[16:17], v[18:19], v[16:17], v[48:49] op_sel_hi:[1,0,1]
	v_xor_b32_e32 v48, 0x80000000, v83
	v_mov_b32_e32 v49, v83
	v_pk_mul_f32 v[48:49], v[48:49], v[16:17] op_sel:[0,1] op_sel_hi:[1,0]
	s_nop 0
	v_pk_fma_f32 v[48:49], v[82:83], v[16:17], v[48:49] op_sel_hi:[0,1,1]
	ds_write_b64 v13, v[48:49] offset:46464
	v_xor_b32_e32 v48, 0x80000000, v17
	v_mov_b32_e32 v49, v17
	v_pk_mul_f32 v[48:49], v[18:19], v[48:49] op_sel:[1,0] op_sel_hi:[0,1]
	v_pk_fma_f32 v[16:17], v[18:19], v[16:17], v[48:49] op_sel_hi:[1,0,1]
	v_xor_b32_e32 v48, 0x80000000, v43
	v_mov_b32_e32 v49, v43
	v_pk_mul_f32 v[48:49], v[48:49], v[16:17] op_sel:[0,1] op_sel_hi:[1,0]
	s_nop 0
	v_pk_fma_f32 v[42:43], v[42:43], v[16:17], v[48:49] op_sel_hi:[0,1,1]
	ds_write_b64 v13, v[42:43] offset:50688
	v_xor_b32_e32 v42, 0x80000000, v17
	v_mov_b32_e32 v43, v17
	v_pk_mul_f32 v[42:43], v[18:19], v[42:43] op_sel:[1,0] op_sel_hi:[0,1]
	v_pk_fma_f32 v[16:17], v[18:19], v[16:17], v[42:43] op_sel_hi:[1,0,1]
	v_xor_b32_e32 v42, 0x80000000, v73
	v_mov_b32_e32 v43, v73
	v_pk_mul_f32 v[42:43], v[42:43], v[16:17] op_sel:[0,1] op_sel_hi:[1,0]
	s_nop 0
	v_pk_fma_f32 v[42:43], v[72:73], v[16:17], v[42:43] op_sel_hi:[0,1,1]
	ds_write_b64 v13, v[42:43] offset:54912
	v_xor_b32_e32 v42, 0x80000000, v17
	v_mov_b32_e32 v43, v17
	v_pk_mul_f32 v[42:43], v[18:19], v[42:43] op_sel:[1,0] op_sel_hi:[0,1]
	v_pk_fma_f32 v[16:17], v[18:19], v[16:17], v[42:43] op_sel_hi:[1,0,1]
	v_xor_b32_e32 v42, 0x80000000, v47
	v_mov_b32_e32 v43, v47
	v_pk_mul_f32 v[42:43], v[42:43], v[16:17] op_sel:[0,1] op_sel_hi:[1,0]
	s_nop 0
	v_pk_fma_f32 v[42:43], v[46:47], v[16:17], v[42:43] op_sel_hi:[0,1,1]
	ds_write_b64 v13, v[42:43] offset:59136
	v_xor_b32_e32 v42, 0x80000000, v17
	v_mov_b32_e32 v43, v17
	v_pk_mul_f32 v[42:43], v[18:19], v[42:43] op_sel:[1,0] op_sel_hi:[0,1]
	v_pk_fma_f32 v[16:17], v[18:19], v[16:17], v[42:43] op_sel_hi:[1,0,1]
	v_xor_b32_e32 v42, 0x80000000, v67
	v_mov_b32_e32 v43, v67
	v_pk_mul_f32 v[42:43], v[42:43], v[16:17] op_sel:[0,1] op_sel_hi:[1,0]
	s_nop 0
	v_pk_fma_f32 v[42:43], v[66:67], v[16:17], v[42:43] op_sel_hi:[0,1,1]
	ds_write_b64 v13, v[42:43] offset:63360
	v_xor_b32_e32 v42, 0x80000000, v17
	v_mov_b32_e32 v43, v17
	v_pk_mul_f32 v[42:43], v[18:19], v[42:43] op_sel:[1,0] op_sel_hi:[0,1]
	v_pk_fma_f32 v[16:17], v[18:19], v[16:17], v[42:43] op_sel_hi:[1,0,1]
	v_sub_f32_e32 v10, v34, v35
	v_pk_mul_f32 v[34:35], v[16:17], s[44:45]
	s_nop 0
	v_pk_fma_f32 v[34:35], v[10:11], v[16:17], v[34:35] op_sel:[0,0,1] op_sel_hi:[0,1,0]
	v_add_u32_e32 v10, 0x10800, v13
	ds_write_b64 v10, v[34:35]
	v_xor_b32_e32 v34, 0x80000000, v17
	v_mov_b32_e32 v35, v17
	v_pk_mul_f32 v[34:35], v[18:19], v[34:35] op_sel:[1,0] op_sel_hi:[0,1]
	v_pk_fma_f32 v[16:17], v[18:19], v[16:17], v[34:35] op_sel_hi:[1,0,1]
	v_xor_b32_e32 v34, 0x80000000, v55
	v_mov_b32_e32 v35, v55
	v_pk_mul_f32 v[34:35], v[34:35], v[16:17] op_sel:[0,1] op_sel_hi:[1,0]
	v_add_u32_e32 v10, 0x11880, v13
	v_pk_fma_f32 v[34:35], v[54:55], v[16:17], v[34:35] op_sel_hi:[0,1,1]
	ds_write_b64 v10, v[34:35]
	v_xor_b32_e32 v34, 0x80000000, v17
	v_mov_b32_e32 v35, v17
	v_pk_mul_f32 v[34:35], v[18:19], v[34:35] op_sel:[1,0] op_sel_hi:[0,1]
	v_pk_fma_f32 v[16:17], v[18:19], v[16:17], v[34:35] op_sel_hi:[1,0,1]
	v_xor_b32_e32 v34, 0x80000000, v39
	v_mov_b32_e32 v35, v39
	v_pk_mul_f32 v[34:35], v[34:35], v[16:17] op_sel:[0,1] op_sel_hi:[1,0]
	v_add_u32_e32 v10, 0x12900, v13
	v_pk_fma_f32 v[34:35], v[38:39], v[16:17], v[34:35] op_sel_hi:[0,1,1]
	ds_write_b64 v10, v[34:35]
	v_xor_b32_e32 v34, 0x80000000, v17
	v_mov_b32_e32 v35, v17
	v_pk_mul_f32 v[34:35], v[18:19], v[34:35] op_sel:[1,0] op_sel_hi:[0,1]
	v_pk_fma_f32 v[16:17], v[18:19], v[16:17], v[34:35] op_sel_hi:[1,0,1]
	v_xor_b32_e32 v34, 0x80000000, v57
	v_mov_b32_e32 v35, v57
	v_pk_mul_f32 v[34:35], v[34:35], v[16:17] op_sel:[0,1] op_sel_hi:[1,0]
	v_add_u32_e32 v10, 0x13980, v13
	v_pk_fma_f32 v[34:35], v[56:57], v[16:17], v[34:35] op_sel_hi:[0,1,1]
	ds_write_b64 v10, v[34:35]
	v_xor_b32_e32 v34, 0x80000000, v17
	v_mov_b32_e32 v35, v17
	v_pk_mul_f32 v[34:35], v[18:19], v[34:35] op_sel:[1,0] op_sel_hi:[0,1]
	v_pk_fma_f32 v[16:17], v[18:19], v[16:17], v[34:35] op_sel_hi:[1,0,1]
	v_xor_b32_e32 v34, 0x80000000, v31
	v_mov_b32_e32 v35, v31
	v_pk_mul_f32 v[34:35], v[34:35], v[16:17] op_sel:[0,1] op_sel_hi:[1,0]
	v_add_u32_e32 v10, 0x14a00, v13
	v_pk_fma_f32 v[30:31], v[30:31], v[16:17], v[34:35] op_sel_hi:[0,1,1]
	ds_write_b64 v10, v[30:31]
	v_xor_b32_e32 v30, 0x80000000, v17
	v_mov_b32_e32 v31, v17
	v_pk_mul_f32 v[30:31], v[18:19], v[30:31] op_sel:[1,0] op_sel_hi:[0,1]
	v_pk_fma_f32 v[16:17], v[18:19], v[16:17], v[30:31] op_sel_hi:[1,0,1]
	v_xor_b32_e32 v30, 0x80000000, v51
	v_mov_b32_e32 v31, v51
	v_pk_mul_f32 v[30:31], v[30:31], v[16:17] op_sel:[0,1] op_sel_hi:[1,0]
	v_add_u32_e32 v10, 0x15a80, v13
	v_pk_fma_f32 v[30:31], v[50:51], v[16:17], v[30:31] op_sel_hi:[0,1,1]
	ds_write_b64 v10, v[30:31]
	v_xor_b32_e32 v30, 0x80000000, v17
	v_mov_b32_e32 v31, v17
	v_pk_mul_f32 v[30:31], v[18:19], v[30:31] op_sel:[1,0] op_sel_hi:[0,1]
	v_pk_fma_f32 v[16:17], v[18:19], v[16:17], v[30:31] op_sel_hi:[1,0,1]
	v_xor_b32_e32 v30, 0x80000000, v33
	v_mov_b32_e32 v31, v33
	v_pk_mul_f32 v[30:31], v[30:31], v[16:17] op_sel:[0,1] op_sel_hi:[1,0]
	v_add_u32_e32 v10, 0x16b00, v13
	v_pk_fma_f32 v[30:31], v[32:33], v[16:17], v[30:31] op_sel_hi:[0,1,1]
	ds_write_b64 v10, v[30:31]
	v_xor_b32_e32 v30, 0x80000000, v17
	v_mov_b32_e32 v31, v17
	v_pk_mul_f32 v[30:31], v[18:19], v[30:31] op_sel:[1,0] op_sel_hi:[0,1]
	v_pk_fma_f32 v[16:17], v[18:19], v[16:17], v[30:31] op_sel_hi:[1,0,1]
	v_xor_b32_e32 v30, 0x80000000, v53
	v_mov_b32_e32 v31, v53
	v_pk_mul_f32 v[30:31], v[30:31], v[16:17] op_sel:[0,1] op_sel_hi:[1,0]
	v_add_u32_e32 v10, 0x17b80, v13
	v_pk_fma_f32 v[30:31], v[52:53], v[16:17], v[30:31] op_sel_hi:[0,1,1]
	ds_write_b64 v10, v[30:31]
	v_xor_b32_e32 v30, 0x80000000, v17
	v_mov_b32_e32 v31, v17
	v_pk_mul_f32 v[30:31], v[18:19], v[30:31] op_sel:[1,0] op_sel_hi:[0,1]
	v_pk_fma_f32 v[16:17], v[18:19], v[16:17], v[30:31] op_sel_hi:[1,0,1]
	v_xor_b32_e32 v30, 0x80000000, v25
	v_mov_b32_e32 v31, v25
	v_pk_mul_f32 v[30:31], v[30:31], v[16:17] op_sel:[0,1] op_sel_hi:[1,0]
	v_add_u32_e32 v10, 0x18c00, v13
	v_pk_fma_f32 v[24:25], v[24:25], v[16:17], v[30:31] op_sel_hi:[0,1,1]
	ds_write_b64 v10, v[24:25]
	v_xor_b32_e32 v24, 0x80000000, v17
	v_mov_b32_e32 v25, v17
	v_pk_mul_f32 v[24:25], v[18:19], v[24:25] op_sel:[1,0] op_sel_hi:[0,1]
	v_pk_fma_f32 v[16:17], v[18:19], v[16:17], v[24:25] op_sel_hi:[1,0,1]
	v_xor_b32_e32 v24, 0x80000000, v41
	v_mov_b32_e32 v25, v41
	v_pk_mul_f32 v[24:25], v[24:25], v[16:17] op_sel:[0,1] op_sel_hi:[1,0]
	v_add_u32_e32 v10, 0x19c80, v13
	v_pk_fma_f32 v[24:25], v[40:41], v[16:17], v[24:25] op_sel_hi:[0,1,1]
	ds_write_b64 v10, v[24:25]
	v_xor_b32_e32 v24, 0x80000000, v17
	v_mov_b32_e32 v25, v17
	v_pk_mul_f32 v[24:25], v[18:19], v[24:25] op_sel:[1,0] op_sel_hi:[0,1]
	v_pk_fma_f32 v[16:17], v[18:19], v[16:17], v[24:25] op_sel_hi:[1,0,1]
	v_xor_b32_e32 v24, 0x80000000, v27
	v_mov_b32_e32 v25, v27
	v_pk_mul_f32 v[24:25], v[24:25], v[16:17] op_sel:[0,1] op_sel_hi:[1,0]
	v_add_u32_e32 v10, 0x1ad00, v13
	v_pk_fma_f32 v[24:25], v[26:27], v[16:17], v[24:25] op_sel_hi:[0,1,1]
	ds_write_b64 v10, v[24:25]
	v_xor_b32_e32 v24, 0x80000000, v17
	v_mov_b32_e32 v25, v17
	v_pk_mul_f32 v[24:25], v[18:19], v[24:25] op_sel:[1,0] op_sel_hi:[0,1]
	v_pk_fma_f32 v[16:17], v[18:19], v[16:17], v[24:25] op_sel_hi:[1,0,1]
	v_xor_b32_e32 v24, 0x80000000, v45
	v_mov_b32_e32 v25, v45
	v_pk_mul_f32 v[24:25], v[24:25], v[16:17] op_sel:[0,1] op_sel_hi:[1,0]
	v_add_u32_e32 v10, 0x1bd80, v13
	v_pk_fma_f32 v[24:25], v[44:45], v[16:17], v[24:25] op_sel_hi:[0,1,1]
	ds_write_b64 v10, v[24:25]
	v_xor_b32_e32 v24, 0x80000000, v17
	v_mov_b32_e32 v25, v17
	v_pk_mul_f32 v[24:25], v[18:19], v[24:25] op_sel:[1,0] op_sel_hi:[0,1]
	v_pk_fma_f32 v[16:17], v[18:19], v[16:17], v[24:25] op_sel_hi:[1,0,1]
	v_xor_b32_e32 v24, 0x80000000, v21
	v_mov_b32_e32 v25, v21
	v_pk_mul_f32 v[24:25], v[24:25], v[16:17] op_sel:[0,1] op_sel_hi:[1,0]
	v_add_u32_e32 v10, 0x1ce00, v13
	v_pk_fma_f32 v[20:21], v[20:21], v[16:17], v[24:25] op_sel_hi:[0,1,1]
	ds_write_b64 v10, v[20:21]
	v_xor_b32_e32 v20, 0x80000000, v17
	v_mov_b32_e32 v21, v17
	v_pk_mul_f32 v[20:21], v[18:19], v[20:21] op_sel:[1,0] op_sel_hi:[0,1]
	v_pk_fma_f32 v[16:17], v[18:19], v[16:17], v[20:21] op_sel_hi:[1,0,1]
	v_xor_b32_e32 v20, 0x80000000, v37
	v_mov_b32_e32 v21, v37
	v_pk_mul_f32 v[20:21], v[20:21], v[16:17] op_sel:[0,1] op_sel_hi:[1,0]
	v_add_u32_e32 v10, 0x1de80, v13
	v_pk_fma_f32 v[20:21], v[36:37], v[16:17], v[20:21] op_sel_hi:[0,1,1]
	ds_write_b64 v10, v[20:21]
	v_xor_b32_e32 v20, 0x80000000, v17
	v_mov_b32_e32 v21, v17
	v_pk_mul_f32 v[20:21], v[18:19], v[20:21] op_sel:[1,0] op_sel_hi:[0,1]
	v_pk_fma_f32 v[16:17], v[18:19], v[16:17], v[20:21] op_sel_hi:[1,0,1]
	v_xor_b32_e32 v20, 0x80000000, v23
	v_mov_b32_e32 v21, v23
	v_pk_mul_f32 v[20:21], v[20:21], v[16:17] op_sel:[0,1] op_sel_hi:[1,0]
	v_add_u32_e32 v10, 0x1ef00, v13
	v_pk_fma_f32 v[20:21], v[22:23], v[16:17], v[20:21] op_sel_hi:[0,1,1]
	ds_write_b64 v10, v[20:21]
	v_xor_b32_e32 v20, 0x80000000, v17
	v_mov_b32_e32 v21, v17
	v_pk_mul_f32 v[20:21], v[18:19], v[20:21] op_sel:[1,0] op_sel_hi:[0,1]
	v_pk_fma_f32 v[16:17], v[18:19], v[16:17], v[20:21] op_sel_hi:[1,0,1]
	v_xor_b32_e32 v18, 0x80000000, v29
	v_mov_b32_e32 v19, v29
	v_pk_mul_f32 v[18:19], v[18:19], v[16:17] op_sel:[0,1] op_sel_hi:[1,0]
	v_add_u32_e32 v10, 0x1ff80, v13
	v_pk_fma_f32 v[16:17], v[28:29], v[16:17], v[18:19] op_sel_hi:[0,1,1]
	ds_write_b64 v10, v[16:17]
	v_mov_b32_e32 v10, v174
	v_mov_b32_e32 v13, v172
	s_waitcnt lgkmcnt(0)
	s_barrier
	v_mov_b32_e32 v16, v180
	v_add_u32_e32 v15, v13, v10
	v_lshl_add_u32 v75, v15, 3, 0
	v_xad_u32 v15, v13, 1, v10
	v_lshl_add_u32 v74, v15, 3, 0
	v_xad_u32 v15, v13, 2, v10
	v_lshl_add_u32 v73, v15, 3, 0
	v_xad_u32 v15, v13, 3, v10
	v_lshl_add_u32 v72, v15, 3, 0
	v_xad_u32 v15, v13, 4, v10
	v_lshl_add_u32 v71, v15, 3, 0
	v_xad_u32 v15, v13, 5, v10
	v_lshl_add_u32 v70, v15, 3, 0
	v_xad_u32 v15, v13, 6, v10
	v_lshl_add_u32 v69, v15, 3, 0
	v_xad_u32 v15, v13, 7, v10
	v_lshl_add_u32 v68, v15, 3, 0
	v_xad_u32 v15, v13, 8, v10
	v_lshl_add_u32 v15, v15, 3, 0
	v_add_u32_e32 v67, 0x800, v15
	v_xad_u32 v15, v13, 9, v10
	v_lshl_add_u32 v15, v15, 3, 0
	v_add_u32_e32 v66, 0x800, v15
	v_xad_u32 v15, v13, 10, v10
	v_lshl_add_u32 v15, v15, 3, 0
	v_add_u32_e32 v65, 0x800, v15
	v_xad_u32 v15, v13, 11, v10
	v_lshl_add_u32 v15, v15, 3, 0
	v_add_u32_e32 v64, 0x800, v15
	v_xad_u32 v15, v13, 12, v10
	v_mov_b32_e32 v17, v181
	v_lshl_add_u32 v15, v15, 3, 0
	ds_read2_b64 v[18:21], v75 offset1:16
	ds_read2_b64 v[40:43], v67 offset1:16
	v_add_u32_e32 v63, 0x800, v15
	v_xad_u32 v15, v13, 13, v10
	v_lshl_add_u32 v15, v15, 3, 0
	v_add_u32_e32 v62, 0x800, v15
	v_xad_u32 v15, v13, 14, v10
	v_xad_u32 v10, v13, 15, v10
	ds_read2_b64 v[22:25], v74 offset0:32 offset1:48
	ds_read2_b64 v[48:51], v66 offset0:32 offset1:48
	v_lshl_add_u32 v15, v15, 3, 0
	v_lshl_add_u32 v10, v10, 3, 0
	v_add_u32_e32 v15, 0x800, v15
	v_add_u32_e32 v13, 0x800, v10
	v_mov_b32_e32 v10, v1
	ds_read2_b64 v[26:29], v73 offset0:64 offset1:80
	ds_read2_b64 v[58:61], v72 offset0:96 offset1:112
	ds_read2_b64 v[76:79], v71 offset0:128 offset1:144
	ds_read2_b64 v[80:83], v70 offset0:160 offset1:176
	ds_read2_b64 v[84:87], v69 offset0:192 offset1:208
	ds_read2_b64 v[88:91], v68 offset0:224 offset1:240
	ds_read2_b64 v[54:57], v65 offset0:64 offset1:80
	ds_read2_b64 v[92:95], v64 offset0:96 offset1:112
	ds_read2_b64 v[96:99], v63 offset0:128 offset1:144
	ds_read2_b64 v[100:103], v62 offset0:160 offset1:176
	ds_read2_b64 v[104:107], v15 offset0:192 offset1:208
	ds_read2_b64 v[108:111], v13 offset0:224 offset1:240
	s_waitcnt lgkmcnt(14)
	v_pk_add_f32 v[112:113], v[18:19], v[40:41]
	v_pk_add_f32 v[40:41], v[18:19], v[40:41] neg_lo:[0,1] neg_hi:[0,1]
	v_pk_add_f32 v[18:19], v[20:21], v[42:43]
	v_pk_add_f32 v[20:21], v[20:21], v[42:43] neg_lo:[0,1] neg_hi:[0,1]
	v_mov_b32_e32 v30, v164
	v_mov_b32_e32 v32, v165
	v_mov_b32_e32 v34, v166
	v_mov_b32_e32 v10, v167
	v_mov_b32_e32 v38, v168
	v_mov_b32_e32 v36, v169
	v_mov_b32_e32 v46, v170
	v_xor_b32_e32 v42, 0x80000000, v21
	v_mov_b32_e32 v43, v20
	v_mov_b32_e32 v31, v171
	v_pk_mul_f32 v[42:43], v[42:43], v[46:47] op_sel_hi:[1,0] neg_lo:[0,1] neg_hi:[0,1]
	s_nop 0
	v_pk_fma_f32 v[44:45], v[20:21], v[30:31], v[42:43] op_sel_hi:[1,0,1]
	s_waitcnt lgkmcnt(12)
	v_pk_add_f32 v[20:21], v[22:23], v[48:49]
	v_pk_add_f32 v[22:23], v[22:23], v[48:49] neg_lo:[0,1] neg_hi:[0,1]
	s_nop 0
	v_xor_b32_e32 v42, 0x80000000, v23
	v_mov_b32_e32 v43, v22
	v_pk_mul_f32 v[42:43], v[42:43], v[36:37] op_sel_hi:[1,0] neg_lo:[0,1] neg_hi:[0,1]
	s_nop 0
	v_pk_fma_f32 v[48:49], v[22:23], v[32:33], v[42:43] op_sel_hi:[1,0,1]
	v_pk_add_f32 v[22:23], v[24:25], v[50:51]
	v_pk_add_f32 v[24:25], v[24:25], v[50:51] neg_lo:[0,1] neg_hi:[0,1]
	s_nop 0
	v_xor_b32_e32 v42, 0x80000000, v25
	v_mov_b32_e32 v43, v24
	v_pk_mul_f32 v[42:43], v[42:43], v[38:39] op_sel_hi:[1,0] neg_lo:[0,1] neg_hi:[0,1]
	s_nop 0
	v_pk_fma_f32 v[52:53], v[24:25], v[34:35], v[42:43] op_sel_hi:[1,0,1]
	s_waitcnt lgkmcnt(5)
	v_pk_add_f32 v[24:25], v[26:27], v[54:55]
	v_pk_add_f32 v[26:27], v[26:27], v[54:55] neg_lo:[0,1] neg_hi:[0,1]
	s_nop 0
	v_xor_b32_e32 v42, 0x80000000, v27
	v_mov_b32_e32 v43, v26
	v_pk_mul_f32 v[42:43], v[42:43], v[10:11] op_sel_hi:[1,0] neg_lo:[0,1] neg_hi:[0,1]
	s_nop 0
	v_pk_fma_f32 v[54:55], v[26:27], v[10:11], v[42:43] op_sel_hi:[1,0,1]
	v_pk_add_f32 v[26:27], v[28:29], v[56:57]
	v_pk_add_f32 v[28:29], v[28:29], v[56:57] neg_lo:[0,1] neg_hi:[0,1]
	s_nop 0
	v_pk_mul_f32 v[42:43], v[28:29], v[38:39] op_sel_hi:[1,0]
	v_xor_b32_e32 v50, 0x80000000, v29
	v_mov_b32_e32 v51, v28
	v_pk_fma_f32 v[56:57], v[50:51], v[34:35], v[42:43] op_sel_hi:[1,0,1] neg_lo:[0,1,0] neg_hi:[0,1,0]
	s_waitcnt lgkmcnt(4)
	v_pk_add_f32 v[42:43], v[58:59], v[92:93] neg_lo:[0,1] neg_hi:[0,1]
	v_pk_add_f32 v[28:29], v[58:59], v[92:93]
	v_pk_mul_f32 v[50:51], v[42:43], v[36:37] op_sel_hi:[1,0]
	v_xor_b32_e32 v58, 0x80000000, v43
	v_mov_b32_e32 v59, v42
	v_pk_fma_f32 v[58:59], v[58:59], v[32:33], v[50:51] op_sel_hi:[1,0,1] neg_lo:[0,1,0] neg_hi:[0,1,0]
	v_pk_add_f32 v[50:51], v[60:61], v[94:95] neg_lo:[0,1] neg_hi:[0,1]
	v_pk_add_f32 v[42:43], v[60:61], v[94:95]
	v_pk_mul_f32 v[60:61], v[50:51], v[46:47] op_sel_hi:[1,0]
	v_xor_b32_e32 v92, 0x80000000, v51
	v_mov_b32_e32 v93, v50
	s_waitcnt lgkmcnt(3)
	v_pk_add_f32 v[50:51], v[76:77], v[96:97]
	v_pk_add_f32 v[76:77], v[76:77], v[96:97] neg_lo:[0,1] neg_hi:[0,1]
	v_pk_fma_f32 v[60:61], v[92:93], v[30:31], v[60:61] op_sel_hi:[1,0,1] neg_lo:[0,1,0] neg_hi:[0,1,0]
	v_xor_b32_e32 v93, 0x80000000, v76
	v_mov_b32_e32 v92, v77
	v_pk_add_f32 v[76:77], v[78:79], v[98:99]
	v_pk_add_f32 v[78:79], v[78:79], v[98:99] neg_lo:[0,1] neg_hi:[0,1]
	s_nop 0
	v_pk_mul_f32 v[94:95], v[78:79], v[46:47] op_sel_hi:[1,0] neg_lo:[0,1] neg_hi:[0,1]
	v_xor_b32_e32 v96, 0x80000000, v79
	v_mov_b32_e32 v97, v78
	v_pk_fma_f32 v[78:79], v[96:97], v[30:31], v[94:95] op_sel_hi:[1,0,1] neg_lo:[0,1,0] neg_hi:[0,1,0]
	s_waitcnt lgkmcnt(2)
	v_pk_add_f32 v[94:95], v[80:81], v[100:101]
	v_pk_add_f32 v[80:81], v[80:81], v[100:101] neg_lo:[0,1] neg_hi:[0,1]
	s_nop 0
	v_pk_mul_f32 v[96:97], v[80:81], v[36:37] op_sel_hi:[1,0] neg_lo:[0,1] neg_hi:[0,1]
	v_xor_b32_e32 v98, 0x80000000, v81
	v_mov_b32_e32 v99, v80
	v_pk_fma_f32 v[80:81], v[98:99], v[32:33], v[96:97] op_sel_hi:[1,0,1] neg_lo:[0,1,0] neg_hi:[0,1,0]
	v_pk_add_f32 v[96:97], v[82:83], v[102:103]
	v_pk_add_f32 v[82:83], v[82:83], v[102:103] neg_lo:[0,1] neg_hi:[0,1]
	s_nop 0
	v_pk_mul_f32 v[98:99], v[82:83], v[38:39] op_sel_hi:[1,0] neg_lo:[0,1] neg_hi:[0,1]
	v_xor_b32_e32 v100, 0x80000000, v83
	v_mov_b32_e32 v101, v82
	v_pk_fma_f32 v[82:83], v[100:101], v[34:35], v[98:99] op_sel_hi:[1,0,1] neg_lo:[0,1,0] neg_hi:[0,1,0]
	s_waitcnt lgkmcnt(1)
	v_pk_add_f32 v[98:99], v[84:85], v[104:105]
	v_pk_add_f32 v[84:85], v[84:85], v[104:105] neg_lo:[0,1] neg_hi:[0,1]
	s_nop 0
	v_xor_b32_e32 v100, 0x80000000, v85
	v_mov_b32_e32 v101, v84
	v_pk_mul_f32 v[100:101], v[100:101], v[10:11] op_sel_hi:[1,0] neg_lo:[0,1] neg_hi:[0,1]
	s_nop 0
	v_pk_fma_f32 v[84:85], v[84:85], v[10:11], v[100:101] op_sel_hi:[1,0,1] neg_lo:[0,1,0] neg_hi:[0,1,0]
	v_pk_add_f32 v[100:101], v[86:87], v[106:107]
	v_pk_add_f32 v[86:87], v[86:87], v[106:107] neg_lo:[0,1] neg_hi:[0,1]
	s_nop 0
	v_xor_b32_e32 v102, 0x80000000, v87
	v_mov_b32_e32 v103, v86
	v_pk_mul_f32 v[38:39], v[102:103], v[38:39] op_sel_hi:[1,0] neg_lo:[0,1] neg_hi:[0,1]
	s_nop 0
	v_pk_fma_f32 v[86:87], v[86:87], v[34:35], v[38:39] op_sel_hi:[1,0,1] neg_lo:[0,1,0] neg_hi:[0,1,0]
	s_waitcnt lgkmcnt(0)
	v_pk_add_f32 v[38:39], v[88:89], v[108:109] neg_lo:[0,1] neg_hi:[0,1]
	v_pk_add_f32 v[34:35], v[88:89], v[108:109]
	v_xor_b32_e32 v88, 0x80000000, v39
	v_mov_b32_e32 v89, v38
	v_pk_mul_f32 v[88:89], v[88:89], v[36:37] op_sel_hi:[1,0] neg_lo:[0,1] neg_hi:[0,1]
	s_nop 0
	v_pk_fma_f32 v[88:89], v[38:39], v[32:33], v[88:89] op_sel_hi:[1,0,1] neg_lo:[0,1,0] neg_hi:[0,1,0]
	v_pk_add_f32 v[38:39], v[90:91], v[110:111]
	v_pk_add_f32 v[90:91], v[90:91], v[110:111] neg_lo:[0,1] neg_hi:[0,1]
	s_nop 0
	v_xor_b32_e32 v102, 0x80000000, v91
	v_mov_b32_e32 v103, v90
	v_pk_mul_f32 v[46:47], v[102:103], v[46:47] op_sel_hi:[1,0] neg_lo:[0,1] neg_hi:[0,1]
	s_nop 0
	v_pk_fma_f32 v[90:91], v[90:91], v[30:31], v[46:47] op_sel_hi:[1,0,1] neg_lo:[0,1,0] neg_hi:[0,1,0]
	v_pk_add_f32 v[46:47], v[18:19], v[76:77]
	v_pk_add_f32 v[18:19], v[18:19], v[76:77] neg_lo:[0,1] neg_hi:[0,1]
	v_pk_add_f32 v[30:31], v[112:113], v[50:51]
	v_xor_b32_e32 v76, 0x80000000, v19
	v_mov_b32_e32 v77, v18
	v_pk_mul_f32 v[76:77], v[76:77], v[36:37] op_sel_hi:[1,0] neg_lo:[0,1] neg_hi:[0,1]
	v_pk_add_f32 v[50:51], v[112:113], v[50:51] neg_lo:[0,1] neg_hi:[0,1]
	v_pk_fma_f32 v[76:77], v[18:19], v[32:33], v[76:77] op_sel_hi:[1,0,1]
	v_pk_add_f32 v[18:19], v[20:21], v[94:95]
	v_pk_add_f32 v[20:21], v[20:21], v[94:95] neg_lo:[0,1] neg_hi:[0,1]
	s_nop 0
	v_xor_b32_e32 v94, 0x80000000, v21
	v_mov_b32_e32 v95, v20
	v_pk_mul_f32 v[94:95], v[94:95], v[10:11] op_sel_hi:[1,0] neg_lo:[0,1] neg_hi:[0,1]
	s_nop 0
	v_pk_fma_f32 v[20:21], v[20:21], v[10:11], v[94:95] op_sel_hi:[1,0,1]
	v_pk_add_f32 v[94:95], v[22:23], v[96:97]
	v_pk_add_f32 v[22:23], v[22:23], v[96:97] neg_lo:[0,1] neg_hi:[0,1]
	s_nop 0
	v_pk_mul_f32 v[96:97], v[22:23], v[36:37] op_sel_hi:[1,0]
	v_xor_b32_e32 v102, 0x80000000, v23
	v_mov_b32_e32 v103, v22
	v_pk_add_f32 v[22:23], v[24:25], v[98:99]
	v_pk_add_f32 v[24:25], v[24:25], v[98:99] neg_lo:[0,1] neg_hi:[0,1]
	v_pk_fma_f32 v[96:97], v[102:103], v[32:33], v[96:97] op_sel_hi:[1,0,1] neg_lo:[0,1,0] neg_hi:[0,1,0]
	v_xor_b32_e32 v99, 0x80000000, v24
	v_mov_b32_e32 v98, v25
	v_pk_add_f32 v[24:25], v[26:27], v[100:101]
	v_pk_add_f32 v[26:27], v[26:27], v[100:101] neg_lo:[0,1] neg_hi:[0,1]
	s_nop 0
	v_pk_mul_f32 v[100:101], v[26:27], v[36:37] op_sel_hi:[1,0] neg_lo:[0,1] neg_hi:[0,1]
	v_xor_b32_e32 v102, 0x80000000, v27
	v_mov_b32_e32 v103, v26
	v_pk_add_f32 v[26:27], v[28:29], v[34:35]
	v_pk_add_f32 v[28:29], v[28:29], v[34:35] neg_lo:[0,1] neg_hi:[0,1]
	v_pk_fma_f32 v[100:101], v[102:103], v[32:33], v[100:101] op_sel_hi:[1,0,1] neg_lo:[0,1,0] neg_hi:[0,1,0]
	v_xor_b32_e32 v34, 0x80000000, v29
	v_mov_b32_e32 v35, v28
	v_pk_mul_f32 v[34:35], v[34:35], v[10:11] op_sel_hi:[1,0] neg_lo:[0,1] neg_hi:[0,1]
	v_pk_add_f32 v[102:103], v[30:31], v[22:23] neg_lo:[0,1] neg_hi:[0,1]
	v_pk_fma_f32 v[28:29], v[28:29], v[10:11], v[34:35] op_sel_hi:[1,0,1] neg_lo:[0,1,0] neg_hi:[0,1,0]
	v_pk_add_f32 v[34:35], v[42:43], v[38:39]
	v_pk_add_f32 v[38:39], v[42:43], v[38:39] neg_lo:[0,1] neg_hi:[0,1]
	s_nop 0
	v_xor_b32_e32 v42, 0x80000000, v39
	v_mov_b32_e32 v43, v38
	v_pk_mul_f32 v[42:43], v[42:43], v[36:37] op_sel_hi:[1,0] neg_lo:[0,1] neg_hi:[0,1]
	s_nop 0
	v_pk_fma_f32 v[42:43], v[38:39], v[32:33], v[42:43] op_sel_hi:[1,0,1] neg_lo:[0,1,0] neg_hi:[0,1,0]
	v_pk_add_f32 v[38:39], v[30:31], v[22:23]
	v_pk_add_f32 v[22:23], v[46:47], v[24:25]
	v_pk_add_f32 v[24:25], v[46:47], v[24:25] neg_lo:[0,1] neg_hi:[0,1]
	s_nop 0
	v_xor_b32_e32 v30, 0x80000000, v25
	v_mov_b32_e32 v31, v24
	v_pk_mul_f32 v[30:31], v[30:31], v[10:11] op_sel_hi:[1,0] neg_lo:[0,1] neg_hi:[0,1]
	s_nop 0
	v_pk_fma_f32 v[24:25], v[24:25], v[10:11], v[30:31] op_sel_hi:[1,0,1]
	v_pk_add_f32 v[30:31], v[18:19], v[26:27]
	v_pk_add_f32 v[18:19], v[18:19], v[26:27] neg_lo:[0,1] neg_hi:[0,1]
	s_nop 0
	v_xor_b32_e32 v27, 0x80000000, v18
	v_mov_b32_e32 v26, v19
	v_pk_add_f32 v[18:19], v[94:95], v[34:35]
	v_pk_add_f32 v[34:35], v[94:95], v[34:35] neg_lo:[0,1] neg_hi:[0,1]
	s_nop 0
	v_xor_b32_e32 v46, 0x80000000, v35
	v_mov_b32_e32 v47, v34
	v_pk_mul_f32 v[46:47], v[46:47], v[10:11] op_sel_hi:[1,0] neg_lo:[0,1] neg_hi:[0,1]
	s_nop 0
	v_pk_fma_f32 v[34:35], v[34:35], v[10:11], v[46:47] op_sel_hi:[1,0,1] neg_lo:[0,1,0] neg_hi:[0,1,0]
	v_pk_add_f32 v[46:47], v[38:39], v[30:31]
	v_pk_add_f32 v[38:39], v[38:39], v[30:31] neg_lo:[0,1] neg_hi:[0,1]
	v_pk_add_f32 v[30:31], v[22:23], v[18:19]
	v_pk_add_f32 v[18:19], v[22:23], v[18:19] neg_lo:[0,1] neg_hi:[0,1]
	v_pk_add_f32 v[94:95], v[46:47], v[30:31]
	v_xor_b32_e32 v23, 0x80000000, v18
	v_mov_b32_e32 v22, v19
	v_pk_add_f32 v[18:19], v[102:103], v[26:27]
	v_pk_add_f32 v[102:103], v[102:103], v[26:27] neg_lo:[0,1] neg_hi:[0,1]
	v_pk_add_f32 v[26:27], v[24:25], v[34:35]
	v_pk_add_f32 v[24:25], v[24:25], v[34:35] neg_lo:[0,1] neg_hi:[0,1]
	v_pk_add_f32 v[30:31], v[46:47], v[30:31] neg_lo:[0,1] neg_hi:[0,1]
	v_xor_b32_e32 v35, 0x80000000, v24
	v_mov_b32_e32 v34, v25
	v_pk_add_f32 v[24:25], v[50:51], v[98:99]
	v_pk_add_f32 v[98:99], v[50:51], v[98:99] neg_lo:[0,1] neg_hi:[0,1]
	v_pk_add_f32 v[50:51], v[76:77], v[100:101] neg_lo:[0,1] neg_hi:[0,1]
	v_pk_add_f32 v[46:47], v[38:39], v[22:23]
	v_pk_add_f32 v[22:23], v[38:39], v[22:23] neg_lo:[0,1] neg_hi:[0,1]
	v_pk_add_f32 v[104:105], v[18:19], v[26:27]
	v_pk_add_f32 v[26:27], v[18:19], v[26:27] neg_lo:[0,1] neg_hi:[0,1]
	v_pk_add_f32 v[38:39], v[102:103], v[34:35]
	v_pk_add_f32 v[18:19], v[102:103], v[34:35] neg_lo:[0,1] neg_hi:[0,1]
	v_pk_add_f32 v[34:35], v[76:77], v[100:101]
	v_xor_b32_e32 v76, 0x80000000, v51
	v_mov_b32_e32 v77, v50
	v_pk_mul_f32 v[76:77], v[10:11], v[76:77] op_sel_hi:[0,1] neg_lo:[1,0] neg_hi:[1,0]
	v_pk_fma_f32 v[76:77], v[10:11], v[50:51], v[76:77] op_sel_hi:[0,1,1]
	v_pk_add_f32 v[50:51], v[20:21], v[28:29]
	v_pk_add_f32 v[20:21], v[20:21], v[28:29] neg_lo:[0,1] neg_hi:[0,1]
	s_nop 0
	v_xor_b32_e32 v29, 0x80000000, v20
	v_mov_b32_e32 v28, v21
	v_pk_add_f32 v[20:21], v[96:97], v[42:43]
	v_pk_add_f32 v[42:43], v[96:97], v[42:43] neg_lo:[0,1] neg_hi:[0,1]
	s_nop 0
	v_xor_b32_e32 v96, 0x80000000, v43
	v_mov_b32_e32 v97, v42
	v_pk_mul_f32 v[96:97], v[10:11], v[96:97] op_sel_hi:[0,1] neg_lo:[1,0] neg_hi:[1,0]
	v_pk_fma_f32 v[42:43], v[10:11], v[42:43], v[96:97] op_sel_hi:[0,1,1] neg_lo:[1,0,0] neg_hi:[1,0,0]
	v_pk_add_f32 v[96:97], v[24:25], v[50:51]
	v_pk_add_f32 v[24:25], v[24:25], v[50:51] neg_lo:[0,1] neg_hi:[0,1]
	v_pk_add_f32 v[50:51], v[34:35], v[20:21]
	v_pk_add_f32 v[20:21], v[34:35], v[20:21] neg_lo:[0,1] neg_hi:[0,1]
	v_pk_add_f32 v[102:103], v[96:97], v[50:51]
	v_xor_b32_e32 v101, 0x80000000, v20
	v_mov_b32_e32 v100, v21
	v_pk_add_f32 v[34:35], v[96:97], v[50:51] neg_lo:[0,1] neg_hi:[0,1]
	v_pk_add_f32 v[20:21], v[98:99], v[28:29]
	v_pk_add_f32 v[96:97], v[98:99], v[28:29] neg_lo:[0,1] neg_hi:[0,1]
	v_pk_add_f32 v[28:29], v[76:77], v[42:43]
	v_pk_add_f32 v[42:43], v[76:77], v[42:43] neg_lo:[0,1] neg_hi:[0,1]
	v_pk_add_f32 v[98:99], v[20:21], v[28:29]
	v_xor_b32_e32 v77, 0x80000000, v42
	v_mov_b32_e32 v76, v43
	v_pk_add_f32 v[28:29], v[20:21], v[28:29] neg_lo:[0,1] neg_hi:[0,1]
	v_pk_add_f32 v[42:43], v[96:97], v[76:77]
	v_pk_add_f32 v[20:21], v[96:97], v[76:77] neg_lo:[0,1] neg_hi:[0,1]
	v_pk_add_f32 v[76:77], v[40:41], v[92:93]
	v_pk_add_f32 v[92:93], v[40:41], v[92:93] neg_lo:[0,1] neg_hi:[0,1]
	v_pk_add_f32 v[40:41], v[44:45], v[78:79]
	v_pk_add_f32 v[44:45], v[44:45], v[78:79] neg_lo:[0,1] neg_hi:[0,1]
	v_pk_add_f32 v[50:51], v[24:25], v[100:101]
	v_xor_b32_e32 v78, 0x80000000, v45
	v_mov_b32_e32 v79, v44
	v_pk_mul_f32 v[78:79], v[36:37], v[78:79] op_sel_hi:[0,1] neg_lo:[1,0] neg_hi:[1,0]
	v_pk_fma_f32 v[44:45], v[32:33], v[44:45], v[78:79] op_sel_hi:[0,1,1]
	v_pk_add_f32 v[78:79], v[48:49], v[80:81]
	v_pk_add_f32 v[48:49], v[48:49], v[80:81] neg_lo:[0,1] neg_hi:[0,1]
	v_pk_add_f32 v[24:25], v[24:25], v[100:101] neg_lo:[0,1] neg_hi:[0,1]
	v_xor_b32_e32 v80, 0x80000000, v49
	v_mov_b32_e32 v81, v48
	v_pk_mul_f32 v[80:81], v[10:11], v[80:81] op_sel_hi:[0,1] neg_lo:[1,0] neg_hi:[1,0]
	v_pk_fma_f32 v[80:81], v[10:11], v[48:49], v[80:81] op_sel_hi:[0,1,1]
	v_pk_add_f32 v[48:49], v[52:53], v[82:83]
	v_pk_add_f32 v[52:53], v[52:53], v[82:83] neg_lo:[0,1] neg_hi:[0,1]
	s_nop 0
	v_xor_b32_e32 v82, 0x80000000, v53
	v_mov_b32_e32 v83, v52
	v_pk_mul_f32 v[82:83], v[32:33], v[82:83] op_sel_hi:[0,1] neg_lo:[1,0] neg_hi:[1,0]
	v_pk_fma_f32 v[52:53], v[36:37], v[52:53], v[82:83] op_sel_hi:[0,1,1]
	v_pk_add_f32 v[82:83], v[54:55], v[84:85]
	v_pk_add_f32 v[54:55], v[54:55], v[84:85] neg_lo:[0,1] neg_hi:[0,1]
	s_nop 0
	v_xor_b32_e32 v85, 0x80000000, v54
	v_mov_b32_e32 v84, v55
	v_pk_add_f32 v[54:55], v[56:57], v[86:87]
	v_pk_add_f32 v[56:57], v[56:57], v[86:87] neg_lo:[0,1] neg_hi:[0,1]
	s_nop 0
	v_xor_b32_e32 v86, 0x80000000, v57
	v_mov_b32_e32 v87, v56
	v_pk_mul_f32 v[86:87], v[32:33], v[86:87] op_sel_hi:[0,1] neg_lo:[1,0] neg_hi:[1,0]
	v_pk_fma_f32 v[56:57], v[36:37], v[56:57], v[86:87] op_sel_hi:[0,1,1] neg_lo:[1,0,0] neg_hi:[1,0,0]
	v_pk_add_f32 v[86:87], v[58:59], v[88:89]
	v_pk_add_f32 v[58:59], v[58:59], v[88:89] neg_lo:[0,1] neg_hi:[0,1]
	s_nop 0
	v_xor_b32_e32 v88, 0x80000000, v59
	v_mov_b32_e32 v89, v58
	v_pk_mul_f32 v[88:89], v[10:11], v[88:89] op_sel_hi:[0,1] neg_lo:[1,0] neg_hi:[1,0]
	v_pk_fma_f32 v[58:59], v[10:11], v[58:59], v[88:89] op_sel_hi:[0,1,1] neg_lo:[1,0,0] neg_hi:[1,0,0]
	v_pk_add_f32 v[88:89], v[60:61], v[90:91]
	v_pk_add_f32 v[60:61], v[60:61], v[90:91] neg_lo:[0,1] neg_hi:[0,1]
	s_nop 0
	v_xor_b32_e32 v90, 0x80000000, v61
	v_mov_b32_e32 v91, v60
	v_pk_mul_f32 v[36:37], v[36:37], v[90:91] op_sel_hi:[0,1] neg_lo:[1,0] neg_hi:[1,0]
	v_pk_fma_f32 v[36:37], v[32:33], v[60:61], v[36:37] op_sel_hi:[0,1,1] neg_lo:[1,0,0] neg_hi:[1,0,0]
	v_pk_add_f32 v[32:33], v[76:77], v[82:83]
	v_pk_add_f32 v[60:61], v[76:77], v[82:83] neg_lo:[0,1] neg_hi:[0,1]
	v_pk_add_f32 v[76:77], v[54:55], v[40:41]
	v_pk_add_f32 v[40:41], v[40:41], v[54:55] neg_lo:[0,1] neg_hi:[0,1]
	s_nop 0
	v_xor_b32_e32 v54, 0x80000000, v41
	v_mov_b32_e32 v55, v40
	v_pk_mul_f32 v[54:55], v[10:11], v[54:55] op_sel_hi:[0,1] neg_lo:[1,0] neg_hi:[1,0]
	v_pk_fma_f32 v[54:55], v[10:11], v[40:41], v[54:55] op_sel_hi:[0,1,1]
	v_pk_add_f32 v[40:41], v[78:79], v[86:87]
	v_pk_add_f32 v[78:79], v[78:79], v[86:87] neg_lo:[0,1] neg_hi:[0,1]
	s_nop 0
	v_xor_b32_e32 v83, 0x80000000, v78
	v_mov_b32_e32 v82, v79
	v_pk_add_f32 v[78:79], v[48:49], v[88:89]
	v_pk_add_f32 v[48:49], v[48:49], v[88:89] neg_lo:[0,1] neg_hi:[0,1]
	v_pk_add_f32 v[88:89], v[76:77], v[78:79]
	v_xor_b32_e32 v86, 0x80000000, v49
	v_mov_b32_e32 v87, v48
	v_pk_mul_f32 v[86:87], v[10:11], v[86:87] op_sel_hi:[0,1] neg_lo:[1,0] neg_hi:[1,0]
	v_pk_fma_f32 v[48:49], v[10:11], v[48:49], v[86:87] op_sel_hi:[0,1,1] neg_lo:[1,0,0] neg_hi:[1,0,0]
	v_pk_add_f32 v[86:87], v[32:33], v[40:41]
	v_pk_add_f32 v[32:33], v[32:33], v[40:41] neg_lo:[0,1] neg_hi:[0,1]
	v_pk_add_f32 v[40:41], v[76:77], v[78:79] neg_lo:[0,1] neg_hi:[0,1]
	v_pk_add_f32 v[78:79], v[86:87], v[88:89] neg_lo:[0,1] neg_hi:[0,1]
	v_xor_b32_e32 v77, 0x80000000, v40
	v_mov_b32_e32 v76, v41
	v_pk_add_f32 v[90:91], v[32:33], v[76:77]
	v_pk_add_f32 v[40:41], v[32:33], v[76:77] neg_lo:[0,1] neg_hi:[0,1]
	v_pk_add_f32 v[76:77], v[54:55], v[48:49]
	v_pk_add_f32 v[48:49], v[54:55], v[48:49] neg_lo:[0,1] neg_hi:[0,1]
	v_pk_add_f32 v[32:33], v[60:61], v[82:83]
	v_pk_add_f32 v[60:61], v[60:61], v[82:83] neg_lo:[0,1] neg_hi:[0,1]
	v_xor_b32_e32 v55, 0x80000000, v48
	v_mov_b32_e32 v54, v49
	v_pk_add_f32 v[82:83], v[32:33], v[76:77]
	v_pk_add_f32 v[48:49], v[32:33], v[76:77] neg_lo:[0,1] neg_hi:[0,1]
	v_pk_add_f32 v[76:77], v[60:61], v[54:55]
	v_pk_add_f32 v[32:33], v[60:61], v[54:55] neg_lo:[0,1] neg_hi:[0,1]
	v_pk_add_f32 v[54:55], v[92:93], v[84:85]
	v_pk_add_f32 v[60:61], v[92:93], v[84:85] neg_lo:[0,1] neg_hi:[0,1]
	v_pk_add_f32 v[84:85], v[56:57], v[44:45]
	v_pk_add_f32 v[44:45], v[44:45], v[56:57] neg_lo:[0,1] neg_hi:[0,1]
	v_pk_add_f32 v[86:87], v[86:87], v[88:89]
	v_xor_b32_e32 v56, 0x80000000, v45
	v_mov_b32_e32 v57, v44
	v_pk_mul_f32 v[56:57], v[10:11], v[56:57] op_sel_hi:[0,1] neg_lo:[1,0] neg_hi:[1,0]
	v_pk_fma_f32 v[56:57], v[10:11], v[44:45], v[56:57] op_sel_hi:[0,1,1]
	v_pk_add_f32 v[44:45], v[80:81], v[58:59]
	v_pk_add_f32 v[58:59], v[80:81], v[58:59] neg_lo:[0,1] neg_hi:[0,1]
	v_xor_b32_e32 v88, 0x80000000, v87
	v_xor_b32_e32 v81, 0x80000000, v58
	v_mov_b32_e32 v80, v59
	v_pk_add_f32 v[58:59], v[52:53], v[36:37]
	v_pk_add_f32 v[36:37], v[52:53], v[36:37] neg_lo:[0,1] neg_hi:[0,1]
	v_mov_b32_e32 v89, v87
	v_xor_b32_e32 v52, 0x80000000, v37
	v_mov_b32_e32 v53, v36
	v_pk_mul_f32 v[52:53], v[10:11], v[52:53] op_sel_hi:[0,1] neg_lo:[1,0] neg_hi:[1,0]
	v_pk_fma_f32 v[36:37], v[10:11], v[36:37], v[52:53] op_sel_hi:[0,1,1] neg_lo:[1,0,0] neg_hi:[1,0,0]
	v_pk_add_f32 v[52:53], v[54:55], v[44:45]
	v_pk_add_f32 v[44:45], v[54:55], v[44:45] neg_lo:[0,1] neg_hi:[0,1]
	v_pk_add_f32 v[54:55], v[84:85], v[58:59]
	v_pk_add_f32 v[58:59], v[84:85], v[58:59] neg_lo:[0,1] neg_hi:[0,1]
	s_nop 0
	v_xor_b32_e32 v85, 0x80000000, v58
	v_mov_b32_e32 v84, v59
	v_pk_add_f32 v[58:59], v[52:53], v[54:55]
	v_pk_add_f32 v[52:53], v[52:53], v[54:55] neg_lo:[0,1] neg_hi:[0,1]
	v_pk_add_f32 v[54:55], v[44:45], v[84:85]
	v_pk_add_f32 v[44:45], v[44:45], v[84:85] neg_lo:[0,1] neg_hi:[0,1]
	v_pk_add_f32 v[84:85], v[60:61], v[80:81]
	v_pk_add_f32 v[60:61], v[60:61], v[80:81] neg_lo:[0,1] neg_hi:[0,1]
	v_pk_add_f32 v[80:81], v[56:57], v[36:37]
	v_pk_add_f32 v[36:37], v[56:57], v[36:37] neg_lo:[0,1] neg_hi:[0,1]
	v_pk_add_f32 v[92:93], v[84:85], v[80:81]
	v_xor_b32_e32 v57, 0x80000000, v36
	v_mov_b32_e32 v56, v37
	v_pk_add_f32 v[80:81], v[84:85], v[80:81] neg_lo:[0,1] neg_hi:[0,1]
	v_pk_add_f32 v[84:85], v[60:61], v[56:57]
	v_pk_add_f32 v[36:37], v[60:61], v[56:57] neg_lo:[0,1] neg_hi:[0,1]
	v_xor_b32_e32 v56, 0x80000000, v95
	v_mov_b32_e32 v57, v95
	v_pk_fma_f32 v[60:61], v[16:17], s[90:91], v[16:17] op_sel:[1,0,0] op_sel_hi:[0,1,1]
	v_pk_mul_f32 v[56:57], v[56:57], s[14:15]
	v_pk_mul_f32 v[88:89], v[60:61], v[88:89] op_sel:[1,0] op_sel_hi:[0,1]
	v_pk_fma_f32 v[56:57], v[94:95], s[94:95], v[56:57] op_sel_hi:[0,1,1]
	v_pk_fma_f32 v[86:87], v[60:61], v[86:87], v[88:89] op_sel_hi:[1,0,1]
	ds_write2_b64 v75, v[56:57], v[86:87] offset1:16
	v_xor_b32_e32 v56, 0x80000000, v61
	v_mov_b32_e32 v57, v61
	v_pk_mul_f32 v[56:57], v[16:17], v[56:57] op_sel:[1,0] op_sel_hi:[0,1]
	v_pk_fma_f32 v[56:57], v[16:17], v[60:61], v[56:57] op_sel_hi:[1,0,1]
	v_xor_b32_e32 v60, 0x80000000, v103
	v_mov_b32_e32 v61, v103
	v_xor_b32_e32 v86, 0x80000000, v57
	v_mov_b32_e32 v87, v57
	v_pk_mul_f32 v[60:61], v[56:57], v[60:61] op_sel:[1,0] op_sel_hi:[0,1]
	v_pk_mul_f32 v[86:87], v[16:17], v[86:87] op_sel:[1,0] op_sel_hi:[0,1]
	v_pk_fma_f32 v[60:61], v[56:57], v[102:103], v[60:61] op_sel_hi:[1,0,1]
	v_pk_fma_f32 v[56:57], v[16:17], v[56:57], v[86:87] op_sel_hi:[1,0,1]
	v_xor_b32_e32 v86, 0x80000000, v59
	v_mov_b32_e32 v87, v59
	v_pk_mul_f32 v[86:87], v[56:57], v[86:87] op_sel:[1,0] op_sel_hi:[0,1]
	v_pk_fma_f32 v[58:59], v[56:57], v[58:59], v[86:87] op_sel_hi:[1,0,1]
	ds_write2_b64 v74, v[60:61], v[58:59] offset0:32 offset1:48
	v_xor_b32_e32 v58, 0x80000000, v57
	v_mov_b32_e32 v59, v57
	v_pk_mul_f32 v[58:59], v[16:17], v[58:59] op_sel:[1,0] op_sel_hi:[0,1]
	v_pk_fma_f32 v[56:57], v[16:17], v[56:57], v[58:59] op_sel_hi:[1,0,1]
	v_xor_b32_e32 v58, 0x80000000, v105
	v_mov_b32_e32 v59, v105
	v_xor_b32_e32 v60, 0x80000000, v57
	v_mov_b32_e32 v61, v57
	v_pk_mul_f32 v[58:59], v[56:57], v[58:59] op_sel:[1,0] op_sel_hi:[0,1]
	v_pk_mul_f32 v[60:61], v[16:17], v[60:61] op_sel:[1,0] op_sel_hi:[0,1]
	v_pk_fma_f32 v[58:59], v[56:57], v[104:105], v[58:59] op_sel_hi:[1,0,1]
	v_pk_fma_f32 v[56:57], v[16:17], v[56:57], v[60:61] op_sel_hi:[1,0,1]
	v_xor_b32_e32 v60, 0x80000000, v83
	v_mov_b32_e32 v61, v83
	v_pk_mul_f32 v[60:61], v[56:57], v[60:61] op_sel:[1,0] op_sel_hi:[0,1]
	v_pk_fma_f32 v[60:61], v[56:57], v[82:83], v[60:61] op_sel_hi:[1,0,1]
	ds_write2_b64 v73, v[58:59], v[60:61] offset0:64 offset1:80
	v_xor_b32_e32 v58, 0x80000000, v57
	v_mov_b32_e32 v59, v57
	v_pk_mul_f32 v[58:59], v[16:17], v[58:59] op_sel:[1,0] op_sel_hi:[0,1]
	v_pk_fma_f32 v[56:57], v[16:17], v[56:57], v[58:59] op_sel_hi:[1,0,1]
	v_xor_b32_e32 v58, 0x80000000, v99
	v_mov_b32_e32 v59, v99
	v_xor_b32_e32 v60, 0x80000000, v57
	v_mov_b32_e32 v61, v57
	v_pk_mul_f32 v[58:59], v[56:57], v[58:59] op_sel:[1,0] op_sel_hi:[0,1]
	v_pk_mul_f32 v[60:61], v[16:17], v[60:61] op_sel:[1,0] op_sel_hi:[0,1]
	v_pk_fma_f32 v[58:59], v[56:57], v[98:99], v[58:59] op_sel_hi:[1,0,1]
	v_pk_fma_f32 v[56:57], v[16:17], v[56:57], v[60:61] op_sel_hi:[1,0,1]
	v_xor_b32_e32 v60, 0x80000000, v93
	v_mov_b32_e32 v61, v93
	v_pk_mul_f32 v[60:61], v[56:57], v[60:61] op_sel:[1,0] op_sel_hi:[0,1]
	v_pk_fma_f32 v[60:61], v[56:57], v[92:93], v[60:61] op_sel_hi:[1,0,1]
	ds_write2_b64 v72, v[58:59], v[60:61] offset0:96 offset1:112
	v_xor_b32_e32 v58, 0x80000000, v57
	v_mov_b32_e32 v59, v57
	v_pk_mul_f32 v[58:59], v[16:17], v[58:59] op_sel:[1,0] op_sel_hi:[0,1]
	v_pk_fma_f32 v[56:57], v[16:17], v[56:57], v[58:59] op_sel_hi:[1,0,1]
	v_xor_b32_e32 v58, 0x80000000, v47
	v_mov_b32_e32 v59, v47
	v_pk_mul_f32 v[58:59], v[56:57], v[58:59] op_sel:[1,0] op_sel_hi:[0,1]
	v_pk_fma_f32 v[46:47], v[56:57], v[46:47], v[58:59] op_sel_hi:[1,0,1]
	v_xor_b32_e32 v58, 0x80000000, v57
	v_mov_b32_e32 v59, v57
	v_pk_mul_f32 v[58:59], v[16:17], v[58:59] op_sel:[1,0] op_sel_hi:[0,1]
	v_pk_fma_f32 v[56:57], v[16:17], v[56:57], v[58:59] op_sel_hi:[1,0,1]
	v_xor_b32_e32 v58, 0x80000000, v91
	v_mov_b32_e32 v59, v91
	v_pk_mul_f32 v[58:59], v[56:57], v[58:59] op_sel:[1,0] op_sel_hi:[0,1]
	v_pk_fma_f32 v[58:59], v[56:57], v[90:91], v[58:59] op_sel_hi:[1,0,1]
	ds_write2_b64 v71, v[46:47], v[58:59] offset0:128 offset1:144
	v_xor_b32_e32 v46, 0x80000000, v57
	v_mov_b32_e32 v47, v57
	v_pk_mul_f32 v[46:47], v[16:17], v[46:47] op_sel:[1,0] op_sel_hi:[0,1]
	v_pk_fma_f32 v[46:47], v[16:17], v[56:57], v[46:47] op_sel_hi:[1,0,1]
	v_xor_b32_e32 v56, 0x80000000, v51
	v_mov_b32_e32 v57, v51
	v_pk_mul_f32 v[56:57], v[46:47], v[56:57] op_sel:[1,0] op_sel_hi:[0,1]
	v_pk_fma_f32 v[50:51], v[46:47], v[50:51], v[56:57] op_sel_hi:[1,0,1]
	v_xor_b32_e32 v56, 0x80000000, v47
	v_mov_b32_e32 v57, v47
	v_pk_mul_f32 v[56:57], v[16:17], v[56:57] op_sel:[1,0] op_sel_hi:[0,1]
	v_pk_fma_f32 v[46:47], v[16:17], v[46:47], v[56:57] op_sel_hi:[1,0,1]
	v_xor_b32_e32 v56, 0x80000000, v55
	v_mov_b32_e32 v57, v55
	v_pk_mul_f32 v[56:57], v[46:47], v[56:57] op_sel:[1,0] op_sel_hi:[0,1]
	v_pk_fma_f32 v[54:55], v[46:47], v[54:55], v[56:57] op_sel_hi:[1,0,1]
	ds_write2_b64 v70, v[50:51], v[54:55] offset0:160 offset1:176
	v_xor_b32_e32 v50, 0x80000000, v47
	v_mov_b32_e32 v51, v47
	v_pk_mul_f32 v[50:51], v[16:17], v[50:51] op_sel:[1,0] op_sel_hi:[0,1]
	v_pk_fma_f32 v[46:47], v[16:17], v[46:47], v[50:51] op_sel_hi:[1,0,1]
	v_xor_b32_e32 v50, 0x80000000, v39
	v_mov_b32_e32 v51, v39
	v_pk_mul_f32 v[50:51], v[50:51], v[46:47] op_sel:[0,1] op_sel_hi:[1,0]
	s_nop 0
	v_pk_fma_f32 v[38:39], v[38:39], v[46:47], v[50:51] op_sel_hi:[0,1,1]
	v_xor_b32_e32 v50, 0x80000000, v47
	v_mov_b32_e32 v51, v47
	v_pk_mul_f32 v[50:51], v[16:17], v[50:51] op_sel:[1,0] op_sel_hi:[0,1]
	v_pk_fma_f32 v[46:47], v[16:17], v[46:47], v[50:51] op_sel_hi:[1,0,1]
	v_xor_b32_e32 v50, 0x80000000, v77
	v_mov_b32_e32 v51, v77
	v_pk_mul_f32 v[50:51], v[46:47], v[50:51] op_sel:[1,0] op_sel_hi:[0,1]
	v_pk_fma_f32 v[50:51], v[46:47], v[76:77], v[50:51] op_sel_hi:[1,0,1]
	ds_write2_b64 v69, v[38:39], v[50:51] offset0:192 offset1:208
	v_xor_b32_e32 v38, 0x80000000, v47
	v_mov_b32_e32 v39, v47
	v_pk_mul_f32 v[38:39], v[16:17], v[38:39] op_sel:[1,0] op_sel_hi:[0,1]
	v_pk_fma_f32 v[38:39], v[16:17], v[46:47], v[38:39] op_sel_hi:[1,0,1]
	v_xor_b32_e32 v46, 0x80000000, v43
	v_mov_b32_e32 v47, v43
	v_pk_mul_f32 v[46:47], v[46:47], v[38:39] op_sel:[0,1] op_sel_hi:[1,0]
	s_nop 0
	v_pk_fma_f32 v[42:43], v[42:43], v[38:39], v[46:47] op_sel_hi:[0,1,1]
	v_xor_b32_e32 v46, 0x80000000, v39
	v_mov_b32_e32 v47, v39
	v_pk_mul_f32 v[46:47], v[16:17], v[46:47] op_sel:[1,0] op_sel_hi:[0,1]
	v_pk_fma_f32 v[38:39], v[16:17], v[38:39], v[46:47] op_sel_hi:[1,0,1]
	v_xor_b32_e32 v46, 0x80000000, v85
	v_mov_b32_e32 v47, v85
	v_pk_mul_f32 v[46:47], v[38:39], v[46:47] op_sel:[1,0] op_sel_hi:[0,1]
	v_pk_fma_f32 v[46:47], v[38:39], v[84:85], v[46:47] op_sel_hi:[1,0,1]
	ds_write2_b64 v68, v[42:43], v[46:47] offset0:224 offset1:240
	v_xor_b32_e32 v42, 0x80000000, v39
	v_mov_b32_e32 v43, v39
	v_pk_mul_f32 v[42:43], v[16:17], v[42:43] op_sel:[1,0] op_sel_hi:[0,1]
	v_pk_fma_f32 v[38:39], v[16:17], v[38:39], v[42:43] op_sel_hi:[1,0,1]
	v_xor_b32_e32 v42, 0x80000000, v31
	v_mov_b32_e32 v43, v31
	v_pk_mul_f32 v[42:43], v[42:43], v[38:39] op_sel:[0,1] op_sel_hi:[1,0]
	s_nop 0
	v_pk_fma_f32 v[30:31], v[30:31], v[38:39], v[42:43] op_sel_hi:[0,1,1]
	v_xor_b32_e32 v42, 0x80000000, v39
	v_mov_b32_e32 v43, v39
	v_pk_mul_f32 v[42:43], v[16:17], v[42:43] op_sel:[1,0] op_sel_hi:[0,1]
	v_pk_fma_f32 v[38:39], v[16:17], v[38:39], v[42:43] op_sel_hi:[1,0,1]
	v_xor_b32_e32 v42, 0x80000000, v79
	v_mov_b32_e32 v43, v79
	v_pk_mul_f32 v[42:43], v[42:43], v[38:39] op_sel:[0,1] op_sel_hi:[1,0]
	s_nop 0
	v_pk_fma_f32 v[42:43], v[78:79], v[38:39], v[42:43] op_sel_hi:[0,1,1]
	ds_write2_b64 v67, v[30:31], v[42:43] offset1:16
	v_xor_b32_e32 v30, 0x80000000, v39
	v_mov_b32_e32 v31, v39
	v_pk_mul_f32 v[30:31], v[16:17], v[30:31] op_sel:[1,0] op_sel_hi:[0,1]
	v_pk_fma_f32 v[30:31], v[16:17], v[38:39], v[30:31] op_sel_hi:[1,0,1]
	v_xor_b32_e32 v38, 0x80000000, v35
	v_mov_b32_e32 v39, v35
	v_pk_mul_f32 v[38:39], v[38:39], v[30:31] op_sel:[0,1] op_sel_hi:[1,0]
	s_nop 0
	v_pk_fma_f32 v[34:35], v[34:35], v[30:31], v[38:39] op_sel_hi:[0,1,1]
	v_xor_b32_e32 v38, 0x80000000, v31
	v_mov_b32_e32 v39, v31
	v_pk_mul_f32 v[38:39], v[16:17], v[38:39] op_sel:[1,0] op_sel_hi:[0,1]
	v_pk_fma_f32 v[30:31], v[16:17], v[30:31], v[38:39] op_sel_hi:[1,0,1]
	v_xor_b32_e32 v38, 0x80000000, v53
	v_mov_b32_e32 v39, v53
	v_pk_mul_f32 v[38:39], v[38:39], v[30:31] op_sel:[0,1] op_sel_hi:[1,0]
	s_nop 0
	v_pk_fma_f32 v[38:39], v[52:53], v[30:31], v[38:39] op_sel_hi:[0,1,1]
	ds_write2_b64 v66, v[34:35], v[38:39] offset0:32 offset1:48
	v_xor_b32_e32 v34, 0x80000000, v31
	v_mov_b32_e32 v35, v31
	v_pk_mul_f32 v[34:35], v[16:17], v[34:35] op_sel:[1,0] op_sel_hi:[0,1]
	v_pk_fma_f32 v[30:31], v[16:17], v[30:31], v[34:35] op_sel_hi:[1,0,1]
	v_xor_b32_e32 v34, 0x80000000, v27
	v_mov_b32_e32 v35, v27
	v_pk_mul_f32 v[34:35], v[34:35], v[30:31] op_sel:[0,1] op_sel_hi:[1,0]
	s_nop 0
	v_pk_fma_f32 v[26:27], v[26:27], v[30:31], v[34:35] op_sel_hi:[0,1,1]
	v_xor_b32_e32 v34, 0x80000000, v31
	v_mov_b32_e32 v35, v31
	v_pk_mul_f32 v[34:35], v[16:17], v[34:35] op_sel:[1,0] op_sel_hi:[0,1]
	v_pk_fma_f32 v[30:31], v[16:17], v[30:31], v[34:35] op_sel_hi:[1,0,1]
	v_xor_b32_e32 v34, 0x80000000, v49
	v_mov_b32_e32 v35, v49
	v_pk_mul_f32 v[34:35], v[34:35], v[30:31] op_sel:[0,1] op_sel_hi:[1,0]
	s_nop 0
	v_pk_fma_f32 v[34:35], v[48:49], v[30:31], v[34:35] op_sel_hi:[0,1,1]
	ds_write2_b64 v65, v[26:27], v[34:35] offset0:64 offset1:80
	v_xor_b32_e32 v26, 0x80000000, v31
	v_mov_b32_e32 v27, v31
	v_pk_mul_f32 v[26:27], v[16:17], v[26:27] op_sel:[1,0] op_sel_hi:[0,1]
	v_pk_fma_f32 v[26:27], v[16:17], v[30:31], v[26:27] op_sel_hi:[1,0,1]
	v_xor_b32_e32 v30, 0x80000000, v29
	v_mov_b32_e32 v31, v29
	v_pk_mul_f32 v[30:31], v[30:31], v[26:27] op_sel:[0,1] op_sel_hi:[1,0]
	s_nop 0
	v_pk_fma_f32 v[28:29], v[28:29], v[26:27], v[30:31] op_sel_hi:[0,1,1]
	v_xor_b32_e32 v30, 0x80000000, v27
	v_mov_b32_e32 v31, v27
	v_pk_mul_f32 v[30:31], v[16:17], v[30:31] op_sel:[1,0] op_sel_hi:[0,1]
	v_pk_fma_f32 v[26:27], v[16:17], v[26:27], v[30:31] op_sel_hi:[1,0,1]
	v_xor_b32_e32 v30, 0x80000000, v81
	v_mov_b32_e32 v31, v81
	v_pk_mul_f32 v[30:31], v[30:31], v[26:27] op_sel:[0,1] op_sel_hi:[1,0]
	s_nop 0
	v_pk_fma_f32 v[30:31], v[80:81], v[26:27], v[30:31] op_sel_hi:[0,1,1]
	ds_write2_b64 v64, v[28:29], v[30:31] offset0:96 offset1:112
	v_xor_b32_e32 v28, 0x80000000, v27
	v_mov_b32_e32 v29, v27
	v_pk_mul_f32 v[28:29], v[16:17], v[28:29] op_sel:[1,0] op_sel_hi:[0,1]
	v_pk_fma_f32 v[26:27], v[16:17], v[26:27], v[28:29] op_sel_hi:[1,0,1]
	v_xor_b32_e32 v28, 0x80000000, v23
	v_mov_b32_e32 v29, v23
	v_pk_mul_f32 v[28:29], v[28:29], v[26:27] op_sel:[0,1] op_sel_hi:[1,0]
	s_nop 0
	v_pk_fma_f32 v[22:23], v[22:23], v[26:27], v[28:29] op_sel_hi:[0,1,1]
	v_xor_b32_e32 v28, 0x80000000, v27
	v_mov_b32_e32 v29, v27
	v_pk_mul_f32 v[28:29], v[16:17], v[28:29] op_sel:[1,0] op_sel_hi:[0,1]
	v_pk_fma_f32 v[26:27], v[16:17], v[26:27], v[28:29] op_sel_hi:[1,0,1]
	v_xor_b32_e32 v28, 0x80000000, v41
	v_mov_b32_e32 v29, v41
	v_pk_mul_f32 v[28:29], v[28:29], v[26:27] op_sel:[0,1] op_sel_hi:[1,0]
	s_nop 0
	v_pk_fma_f32 v[28:29], v[40:41], v[26:27], v[28:29] op_sel_hi:[0,1,1]
	ds_write2_b64 v63, v[22:23], v[28:29] offset0:128 offset1:144
	v_xor_b32_e32 v22, 0x80000000, v27
	v_mov_b32_e32 v23, v27
	v_pk_mul_f32 v[22:23], v[16:17], v[22:23] op_sel:[1,0] op_sel_hi:[0,1]
	v_pk_fma_f32 v[22:23], v[16:17], v[26:27], v[22:23] op_sel_hi:[1,0,1]
	v_xor_b32_e32 v26, 0x80000000, v25
	v_mov_b32_e32 v27, v25
	v_pk_mul_f32 v[26:27], v[26:27], v[22:23] op_sel:[0,1] op_sel_hi:[1,0]
	s_nop 0
	v_pk_fma_f32 v[24:25], v[24:25], v[22:23], v[26:27] op_sel_hi:[0,1,1]
	v_xor_b32_e32 v26, 0x80000000, v23
	v_mov_b32_e32 v27, v23
	v_pk_mul_f32 v[26:27], v[16:17], v[26:27] op_sel:[1,0] op_sel_hi:[0,1]
	v_pk_fma_f32 v[22:23], v[16:17], v[22:23], v[26:27] op_sel_hi:[1,0,1]
	v_xor_b32_e32 v26, 0x80000000, v45
	v_mov_b32_e32 v27, v45
	v_pk_mul_f32 v[26:27], v[26:27], v[22:23] op_sel:[0,1] op_sel_hi:[1,0]
	s_nop 0
	v_pk_fma_f32 v[26:27], v[44:45], v[22:23], v[26:27] op_sel_hi:[0,1,1]
	ds_write2_b64 v62, v[24:25], v[26:27] offset0:160 offset1:176
	v_xor_b32_e32 v24, 0x80000000, v23
	v_mov_b32_e32 v25, v23
	v_pk_mul_f32 v[24:25], v[16:17], v[24:25] op_sel:[1,0] op_sel_hi:[0,1]
	v_pk_fma_f32 v[22:23], v[16:17], v[22:23], v[24:25] op_sel_hi:[1,0,1]
	v_xor_b32_e32 v24, 0x80000000, v19
	v_mov_b32_e32 v25, v19
	v_pk_mul_f32 v[24:25], v[24:25], v[22:23] op_sel:[0,1] op_sel_hi:[1,0]
	s_nop 0
	v_pk_fma_f32 v[18:19], v[18:19], v[22:23], v[24:25] op_sel_hi:[0,1,1]
	v_xor_b32_e32 v24, 0x80000000, v23
	v_mov_b32_e32 v25, v23
	v_pk_mul_f32 v[24:25], v[16:17], v[24:25] op_sel:[1,0] op_sel_hi:[0,1]
	v_pk_fma_f32 v[22:23], v[16:17], v[22:23], v[24:25] op_sel_hi:[1,0,1]
	v_xor_b32_e32 v24, 0x80000000, v33
	v_mov_b32_e32 v25, v33
	v_pk_mul_f32 v[24:25], v[24:25], v[22:23] op_sel:[0,1] op_sel_hi:[1,0]
	s_nop 0
	v_pk_fma_f32 v[24:25], v[32:33], v[22:23], v[24:25] op_sel_hi:[0,1,1]
	ds_write2_b64 v15, v[18:19], v[24:25] offset0:192 offset1:208
	v_xor_b32_e32 v18, 0x80000000, v23
	v_mov_b32_e32 v19, v23
	v_pk_mul_f32 v[18:19], v[16:17], v[18:19] op_sel:[1,0] op_sel_hi:[0,1]
	v_pk_fma_f32 v[18:19], v[16:17], v[22:23], v[18:19] op_sel_hi:[1,0,1]
	v_xor_b32_e32 v22, 0x80000000, v21
	v_mov_b32_e32 v23, v21
	v_pk_mul_f32 v[22:23], v[22:23], v[18:19] op_sel:[0,1] op_sel_hi:[1,0]
	s_nop 0
	v_pk_fma_f32 v[20:21], v[20:21], v[18:19], v[22:23] op_sel_hi:[0,1,1]
	v_xor_b32_e32 v22, 0x80000000, v19
	v_mov_b32_e32 v23, v19
	v_pk_mul_f32 v[22:23], v[16:17], v[22:23] op_sel:[1,0] op_sel_hi:[0,1]
	v_pk_fma_f32 v[16:17], v[16:17], v[18:19], v[22:23] op_sel_hi:[1,0,1]
	v_xor_b32_e32 v18, 0x80000000, v37
	v_mov_b32_e32 v19, v37
	v_pk_mul_f32 v[18:19], v[18:19], v[16:17] op_sel:[0,1] op_sel_hi:[1,0]
	s_nop 0
	v_pk_fma_f32 v[16:17], v[36:37], v[16:17], v[18:19] op_sel_hi:[0,1,1]
	ds_write2_b64 v13, v[20:21], v[16:17] offset0:224 offset1:240
	v_mov_b32_e32 v16, v182
	v_mov_b32_e32 v10, v176
	v_mov_b32_e32 v17, v175
	s_waitcnt lgkmcnt(0)
	s_barrier
	v_lshlrev_b32_e32 v190, 3, v16
	v_add_u32_e32 v190, 0x1000, v190
	global_load_dwordx2 v[202:203], v190, s[46:47] offset:-4096
	global_load_dwordx2 v[204:205], v190, s[46:47]
	v_add_u32_e32 v190, 0x2000, v190
	global_load_dwordx2 v[206:207], v190, s[46:47] offset:-4096
	global_load_dwordx2 v[208:209], v190, s[46:47]
	v_add_u32_e32 v190, 0x2000, v190
	global_load_dwordx2 v[210:211], v190, s[46:47] offset:-4096
	global_load_dwordx2 v[212:213], v190, s[46:47]
	v_add_u32_e32 v190, 0x2000, v190
	global_load_dwordx2 v[214:215], v190, s[46:47] offset:-4096
	global_load_dwordx2 v[216:217], v190, s[46:47]
	v_add_u32_e32 v190, 0x2000, v190
	global_load_dwordx2 v[218:219], v190, s[46:47] offset:-4096
	global_load_dwordx2 v[220:221], v190, s[46:47]
	v_add_u32_e32 v190, 0x2000, v190
	global_load_dwordx2 v[222:223], v190, s[46:47] offset:-4096
	global_load_dwordx2 v[224:225], v190, s[46:47]
	v_add_u32_e32 v190, 0x2000, v190
	global_load_dwordx2 v[226:227], v190, s[46:47] offset:-4096
	global_load_dwordx2 v[228:229], v190, s[46:47]
	v_add_u32_e32 v190, 0x2000, v190
	global_load_dwordx2 v[230:231], v190, s[46:47] offset:-4096
	global_load_dwordx2 v[232:233], v190, s[46:47]
	v_mov_b32_e32 v50, v165
	v_lshlrev_b32_e32 v13, 3, v17
	v_lshlrev_b32_e32 v48, 3, v10
	v_add3_u32 v10, 0, v13, v48
	v_xor_b32_e32 v13, 1, v17
	v_xor_b32_e32 v34, 8, v17
	v_xor_b32_e32 v36, 9, v17
	v_lshlrev_b32_e32 v13, 3, v13
	v_xor_b32_e32 v15, 2, v17
	v_xor_b32_e32 v24, 3, v17
	v_xor_b32_e32 v26, 4, v17
	v_xor_b32_e32 v28, 5, v17
	v_xor_b32_e32 v30, 6, v17
	v_xor_b32_e32 v32, 7, v17
	v_lshlrev_b32_e32 v34, 3, v34
	v_lshlrev_b32_e32 v36, 3, v36
	v_xor_b32_e32 v38, 10, v17
	v_xor_b32_e32 v40, 11, v17
	v_xor_b32_e32 v42, 12, v17
	v_xor_b32_e32 v44, 13, v17
	v_xor_b32_e32 v46, 14, v17
	v_xor_b32_e32 v17, 15, v17
	v_add3_u32 v13, 0, v13, v48
	v_lshlrev_b32_e32 v15, 3, v15
	v_lshlrev_b32_e32 v24, 3, v24
	v_lshlrev_b32_e32 v26, 3, v26
	v_lshlrev_b32_e32 v28, 3, v28
	v_lshlrev_b32_e32 v30, 3, v30
	v_lshlrev_b32_e32 v32, 3, v32
	v_add3_u32 v57, 0, v34, v48
	v_add3_u32 v58, 0, v36, v48
	v_lshlrev_b32_e32 v38, 3, v38
	v_lshlrev_b32_e32 v40, 3, v40
	v_lshlrev_b32_e32 v42, 3, v42
	v_lshlrev_b32_e32 v44, 3, v44
	v_lshlrev_b32_e32 v46, 3, v46
	v_lshlrev_b32_e32 v17, 3, v17
	ds_read_b64 v[18:19], v10
	ds_read_b64 v[20:21], v13
	v_add3_u32 v15, 0, v15, v48
	v_add3_u32 v52, 0, v24, v48
	v_add3_u32 v53, 0, v26, v48
	v_add3_u32 v54, 0, v28, v48
	v_add3_u32 v55, 0, v30, v48
	v_add3_u32 v56, 0, v32, v48
	ds_read_b64 v[34:35], v57
	ds_read_b64 v[36:37], v58
	v_add3_u32 v59, 0, v38, v48
	v_add3_u32 v60, 0, v40, v48
	v_add3_u32 v61, 0, v42, v48
	v_add3_u32 v62, 0, v44, v48
	v_add3_u32 v63, 0, v46, v48
	v_add3_u32 v64, 0, v17, v48
	v_mov_b32_e32 v17, v1
	ds_read_b64 v[22:23], v15
	ds_read_b64 v[24:25], v52
	ds_read_b64 v[26:27], v53
	ds_read_b64 v[28:29], v54
	ds_read_b64 v[30:31], v55
	ds_read_b64 v[32:33], v56
	ds_read_b64 v[38:39], v59
	ds_read_b64 v[40:41], v60
	ds_read_b64 v[42:43], v61
	ds_read_b64 v[44:45], v62
	ds_read_b64 v[46:47], v63
	ds_read_b64 v[48:49], v64
	s_waitcnt lgkmcnt(13)
	v_pk_add_f32 v[70:71], v[18:19], v[34:35]
	v_mov_b32_e32 v17, v164
	v_pk_add_f32 v[18:19], v[18:19], v[34:35] neg_lo:[0,1] neg_hi:[0,1]
	v_mov_b32_e32 v17, v166
	s_waitcnt lgkmcnt(12)
	v_pk_add_f32 v[34:35], v[20:21], v[36:37]
	v_pk_add_f32 v[20:21], v[20:21], v[36:37] neg_lo:[0,1] neg_hi:[0,1]
	v_mov_b32_e32 v66, v167
	v_mov_b32_e32 v17, v168
	v_mov_b32_e32 v68, v169
	v_xor_b32_e32 v36, 0x80000000, v21
	v_mov_b32_e32 v37, v20
	s_nop 0
	v_pk_mul_f32 v[36:37], v[36:37], v[68:69] op_sel_hi:[1,0] neg_lo:[0,1] neg_hi:[0,1]
	v_mov_b32_e32 v17, v170
	v_pk_fma_f32 v[20:21], v[20:21], v[50:51], v[36:37] op_sel_hi:[1,0,1]
	s_waitcnt lgkmcnt(5)
	v_pk_add_f32 v[36:37], v[22:23], v[38:39]
	v_pk_add_f32 v[22:23], v[22:23], v[38:39] neg_lo:[0,1] neg_hi:[0,1]
	s_nop 0
	v_xor_b32_e32 v38, 0x80000000, v23
	v_mov_b32_e32 v39, v22
	v_pk_mul_f32 v[38:39], v[38:39], v[66:67] op_sel_hi:[1,0] neg_lo:[0,1] neg_hi:[0,1]
	v_mov_b32_e32 v17, v171
	v_pk_fma_f32 v[22:23], v[22:23], v[66:67], v[38:39] op_sel_hi:[1,0,1]
	s_waitcnt lgkmcnt(4)
	v_pk_add_f32 v[38:39], v[24:25], v[40:41]
	v_pk_add_f32 v[24:25], v[24:25], v[40:41] neg_lo:[0,1] neg_hi:[0,1]
	s_nop 0
	v_pk_mul_f32 v[40:41], v[24:25], v[68:69] op_sel_hi:[1,0]
	v_xor_b32_e32 v72, 0x80000000, v25
	v_mov_b32_e32 v73, v24
	v_pk_fma_f32 v[24:25], v[72:73], v[50:51], v[40:41] op_sel_hi:[1,0,1] neg_lo:[0,1,0] neg_hi:[0,1,0]
	s_waitcnt lgkmcnt(3)
	v_pk_add_f32 v[40:41], v[26:27], v[42:43]
	v_pk_add_f32 v[26:27], v[26:27], v[42:43] neg_lo:[0,1] neg_hi:[0,1]
	v_ashrrev_i32_e32 v17, 31, v16
	v_xor_b32_e32 v73, 0x80000000, v26
	v_mov_b32_e32 v72, v27
	s_waitcnt lgkmcnt(2)
	v_pk_add_f32 v[26:27], v[28:29], v[44:45]
	v_pk_add_f32 v[28:29], v[28:29], v[44:45] neg_lo:[0,1] neg_hi:[0,1]
	s_nop 0
	v_pk_mul_f32 v[42:43], v[28:29], v[68:69] op_sel_hi:[1,0] neg_lo:[0,1] neg_hi:[0,1]
	v_xor_b32_e32 v44, 0x80000000, v29
	v_mov_b32_e32 v45, v28
	v_pk_fma_f32 v[28:29], v[44:45], v[50:51], v[42:43] op_sel_hi:[1,0,1] neg_lo:[0,1,0] neg_hi:[0,1,0]
	s_waitcnt lgkmcnt(1)
	v_pk_add_f32 v[42:43], v[30:31], v[46:47]
	v_pk_add_f32 v[30:31], v[30:31], v[46:47] neg_lo:[0,1] neg_hi:[0,1]
	s_nop 0
	v_xor_b32_e32 v44, 0x80000000, v31
	v_mov_b32_e32 v45, v30
	v_pk_mul_f32 v[44:45], v[44:45], v[66:67] op_sel_hi:[1,0] neg_lo:[0,1] neg_hi:[0,1]
	s_nop 0
	v_pk_fma_f32 v[30:31], v[30:31], v[66:67], v[44:45] op_sel_hi:[1,0,1] neg_lo:[0,1,0] neg_hi:[0,1,0]
	s_waitcnt lgkmcnt(0)
	v_pk_add_f32 v[44:45], v[32:33], v[48:49]
	v_pk_add_f32 v[32:33], v[32:33], v[48:49] neg_lo:[0,1] neg_hi:[0,1]
	v_pk_add_f32 v[48:49], v[34:35], v[26:27]
	v_pk_add_f32 v[26:27], v[34:35], v[26:27] neg_lo:[0,1] neg_hi:[0,1]
	v_xor_b32_e32 v46, 0x80000000, v33
	v_xor_b32_e32 v34, 0x80000000, v27
	v_mov_b32_e32 v35, v26
	v_pk_mul_f32 v[34:35], v[34:35], v[66:67] op_sel_hi:[1,0] neg_lo:[0,1] neg_hi:[0,1]
	v_mov_b32_e32 v47, v32
	v_pk_fma_f32 v[26:27], v[26:27], v[66:67], v[34:35] op_sel_hi:[1,0,1]
	v_pk_add_f32 v[34:35], v[36:37], v[42:43]
	v_pk_add_f32 v[36:37], v[36:37], v[42:43] neg_lo:[0,1] neg_hi:[0,1]
	v_pk_mul_f32 v[46:47], v[46:47], v[68:69] op_sel_hi:[1,0] neg_lo:[0,1] neg_hi:[0,1]
	v_xor_b32_e32 v43, 0x80000000, v36
	v_mov_b32_e32 v42, v37
	v_pk_add_f32 v[36:37], v[38:39], v[44:45]
	v_pk_add_f32 v[38:39], v[38:39], v[44:45] neg_lo:[0,1] neg_hi:[0,1]
	v_pk_fma_f32 v[46:47], v[32:33], v[50:51], v[46:47] op_sel_hi:[1,0,1] neg_lo:[0,1,0] neg_hi:[0,1,0]
	v_xor_b32_e32 v44, 0x80000000, v39
	v_mov_b32_e32 v45, v38
	v_pk_add_f32 v[32:33], v[70:71], v[40:41]
	v_pk_mul_f32 v[44:45], v[44:45], v[66:67] op_sel_hi:[1,0] neg_lo:[0,1] neg_hi:[0,1]
	v_pk_add_f32 v[40:41], v[70:71], v[40:41] neg_lo:[0,1] neg_hi:[0,1]
	v_pk_fma_f32 v[38:39], v[38:39], v[66:67], v[44:45] op_sel_hi:[1,0,1] neg_lo:[0,1,0] neg_hi:[0,1,0]
	v_pk_add_f32 v[44:45], v[32:33], v[34:35]
	v_pk_add_f32 v[32:33], v[32:33], v[34:35] neg_lo:[0,1] neg_hi:[0,1]
	v_pk_add_f32 v[34:35], v[48:49], v[36:37]
	v_pk_add_f32 v[36:37], v[48:49], v[36:37] neg_lo:[0,1] neg_hi:[0,1]
	v_pk_add_f32 v[50:51], v[44:45], v[34:35]
	v_xor_b32_e32 v49, 0x80000000, v36
	v_mov_b32_e32 v48, v37
	v_pk_add_f32 v[36:37], v[44:45], v[34:35] neg_lo:[0,1] neg_hi:[0,1]
	v_pk_add_f32 v[68:69], v[32:33], v[48:49]
	v_pk_add_f32 v[44:45], v[32:33], v[48:49] neg_lo:[0,1] neg_hi:[0,1]
	v_pk_add_f32 v[32:33], v[40:41], v[42:43]
	v_pk_add_f32 v[34:35], v[40:41], v[42:43] neg_lo:[0,1] neg_hi:[0,1]
	v_pk_add_f32 v[40:41], v[26:27], v[38:39]
	v_pk_add_f32 v[26:27], v[26:27], v[38:39] neg_lo:[0,1] neg_hi:[0,1]
	v_pk_add_f32 v[42:43], v[32:33], v[40:41] neg_lo:[0,1] neg_hi:[0,1]
	v_xor_b32_e32 v39, 0x80000000, v26
	v_mov_b32_e32 v38, v27
	v_pk_add_f32 v[26:27], v[32:33], v[40:41]
	v_pk_add_f32 v[40:41], v[20:21], v[28:29]
	v_pk_add_f32 v[20:21], v[20:21], v[28:29] neg_lo:[0,1] neg_hi:[0,1]
	v_pk_add_f32 v[32:33], v[34:35], v[38:39]
	v_xor_b32_e32 v28, 0x80000000, v21
	v_mov_b32_e32 v29, v20
	v_pk_mul_f32 v[28:29], v[66:67], v[28:29] op_sel_hi:[0,1] neg_lo:[1,0] neg_hi:[1,0]
	v_pk_fma_f32 v[20:21], v[66:67], v[20:21], v[28:29] op_sel_hi:[0,1,1]
	v_pk_add_f32 v[28:29], v[22:23], v[30:31]
	v_pk_add_f32 v[22:23], v[22:23], v[30:31] neg_lo:[0,1] neg_hi:[0,1]
	v_pk_add_f32 v[38:39], v[34:35], v[38:39] neg_lo:[0,1] neg_hi:[0,1]
	v_xor_b32_e32 v31, 0x80000000, v22
	v_mov_b32_e32 v30, v23
	v_pk_add_f32 v[22:23], v[24:25], v[46:47]
	v_pk_add_f32 v[24:25], v[24:25], v[46:47] neg_lo:[0,1] neg_hi:[0,1]
	v_pk_add_f32 v[34:35], v[18:19], v[72:73]
	v_xor_b32_e32 v46, 0x80000000, v25
	v_mov_b32_e32 v47, v24
	v_pk_mul_f32 v[46:47], v[66:67], v[46:47] op_sel_hi:[0,1] neg_lo:[1,0] neg_hi:[1,0]
	v_pk_fma_f32 v[24:25], v[66:67], v[24:25], v[46:47] op_sel_hi:[0,1,1] neg_lo:[1,0,0] neg_hi:[1,0,0]
	v_pk_add_f32 v[46:47], v[34:35], v[28:29]
	v_pk_add_f32 v[28:29], v[34:35], v[28:29] neg_lo:[0,1] neg_hi:[0,1]
	v_pk_add_f32 v[34:35], v[40:41], v[22:23]
	v_pk_add_f32 v[22:23], v[40:41], v[22:23] neg_lo:[0,1] neg_hi:[0,1]
	v_pk_add_f32 v[18:19], v[18:19], v[72:73] neg_lo:[0,1] neg_hi:[0,1]
	v_xor_b32_e32 v49, 0x80000000, v22
	v_mov_b32_e32 v48, v23
	v_pk_add_f32 v[66:67], v[28:29], v[48:49]
	v_pk_add_f32 v[48:49], v[28:29], v[48:49] neg_lo:[0,1] neg_hi:[0,1]
	v_pk_add_f32 v[28:29], v[18:19], v[30:31]
	v_pk_add_f32 v[18:19], v[18:19], v[30:31] neg_lo:[0,1] neg_hi:[0,1]
	v_pk_add_f32 v[30:31], v[20:21], v[24:25]
	v_pk_add_f32 v[20:21], v[20:21], v[24:25] neg_lo:[0,1] neg_hi:[0,1]
	v_pk_add_f32 v[22:23], v[46:47], v[34:35]
	v_xor_b32_e32 v25, 0x80000000, v20
	v_mov_b32_e32 v24, v21
	v_lshl_add_u64 v[20:21], v[16:17], 3, s[46:47]
	s_waitcnt vmcnt(0)
	v_mov_b32_e32 v20, v202
	v_mov_b32_e32 v21, v203
	v_pk_add_f32 v[40:41], v[46:47], v[34:35] neg_lo:[0,1] neg_hi:[0,1]
	v_pk_add_f32 v[34:35], v[18:19], v[24:25]
	v_pk_add_f32 v[18:19], v[18:19], v[24:25] neg_lo:[0,1] neg_hi:[0,1]
	v_xor_b32_e32 v24, 0x80000000, v51
	v_mov_b32_e32 v25, v51
	v_pk_add_f32 v[70:71], v[28:29], v[30:31]
	v_pk_add_f32 v[46:47], v[28:29], v[30:31] neg_lo:[0,1] neg_hi:[0,1]
	v_xor_b32_e32 v28, 0x80000000, v23
	v_mov_b32_e32 v29, v23
	v_xor_b32_e32 v30, 0x80000000, v69
	v_mov_b32_e32 v31, v69
	v_mov_b32_e32 v17, v1
	s_nop 0
	v_pk_mul_f32 v[24:25], v[24:25], v[20:21] op_sel:[0,1] op_sel_hi:[1,0]
	s_nop 0
	v_pk_fma_f32 v[20:21], v[50:51], v[20:21], v[24:25] op_sel_hi:[0,1,1]
	v_add_u32_e32 v24, 0x200, v16
	v_ashrrev_i32_e32 v25, 31, v24
	v_lshl_add_u64 v[24:25], v[24:25], 3, s[46:47]
	v_mov_b32_e32 v24, v204
	v_mov_b32_e32 v25, v205
	v_xor_b32_e32 v50, 0x80000000, v67
	v_mov_b32_e32 v51, v67
	s_nop 0
	v_pk_mul_f32 v[28:29], v[24:25], v[28:29] op_sel:[1,0] op_sel_hi:[0,1]
	v_pk_fma_f32 v[22:23], v[24:25], v[22:23], v[28:29] op_sel_hi:[1,0,1]
	v_add_u32_e32 v24, 0x400, v16
	v_ashrrev_i32_e32 v25, 31, v24
	v_lshl_add_u64 v[24:25], v[24:25], 3, s[46:47]
	v_mov_b32_e32 v24, v206
	v_mov_b32_e32 v25, v207
	v_xor_b32_e32 v28, 0x80000000, v27
	v_mov_b32_e32 v29, v27
	s_nop 0
	v_pk_mul_f32 v[28:29], v[28:29], v[24:25] op_sel:[0,1] op_sel_hi:[1,0]
	s_nop 0
	v_pk_fma_f32 v[24:25], v[26:27], v[24:25], v[28:29] op_sel_hi:[0,1,1]
	v_add_u32_e32 v26, 0x600, v16
	v_ashrrev_i32_e32 v27, 31, v26
	v_lshl_add_u64 v[26:27], v[26:27], 3, s[46:47]
	v_mov_b32_e32 v26, v208
	v_mov_b32_e32 v27, v209
	v_xor_b32_e32 v28, 0x80000000, v71
	v_mov_b32_e32 v29, v71
	s_nop 0
	v_pk_mul_f32 v[28:29], v[26:27], v[28:29] op_sel:[1,0] op_sel_hi:[0,1]
	v_pk_fma_f32 v[26:27], v[26:27], v[70:71], v[28:29] op_sel_hi:[1,0,1]
	v_add_u32_e32 v28, 0x800, v16
	v_ashrrev_i32_e32 v29, 31, v28
	v_lshl_add_u64 v[28:29], v[28:29], 3, s[46:47]
	v_mov_b32_e32 v28, v210
	v_mov_b32_e32 v29, v211
	s_nop 0
	v_pk_mul_f32 v[30:31], v[30:31], v[28:29] op_sel:[0,1] op_sel_hi:[1,0]
	s_nop 0
	v_pk_fma_f32 v[28:29], v[68:69], v[28:29], v[30:31] op_sel_hi:[0,1,1]
	v_add_u32_e32 v30, 0xa00, v16
	v_ashrrev_i32_e32 v31, 31, v30
	v_lshl_add_u64 v[30:31], v[30:31], 3, s[46:47]
	v_mov_b32_e32 v30, v212
	v_mov_b32_e32 v31, v213
	v_mov_b32_e32 v68, v169
	s_nop 0
	v_pk_mul_f32 v[50:51], v[30:31], v[50:51] op_sel:[1,0] op_sel_hi:[0,1]
	v_pk_fma_f32 v[30:31], v[30:31], v[66:67], v[50:51] op_sel_hi:[1,0,1]
	v_add_u32_e32 v50, 0xc00, v16
	v_ashrrev_i32_e32 v51, 31, v50
	v_lshl_add_u64 v[50:51], v[50:51], 3, s[46:47]
	v_mov_b32_e32 v50, v214
	v_mov_b32_e32 v51, v215
	v_xor_b32_e32 v66, 0x80000000, v33
	v_mov_b32_e32 v67, v33
	s_nop 0
	v_pk_mul_f32 v[66:67], v[66:67], v[50:51] op_sel:[0,1] op_sel_hi:[1,0]
	s_nop 0
	v_pk_fma_f32 v[32:33], v[32:33], v[50:51], v[66:67] op_sel_hi:[0,1,1]
	v_add_u32_e32 v50, 0xe00, v16
	v_ashrrev_i32_e32 v51, 31, v50
	v_lshl_add_u64 v[50:51], v[50:51], 3, s[46:47]
	v_mov_b32_e32 v50, v216
	v_mov_b32_e32 v51, v217
	v_xor_b32_e32 v66, 0x80000000, v35
	v_mov_b32_e32 v67, v35
	s_nop 0
	v_pk_mul_f32 v[66:67], v[50:51], v[66:67] op_sel:[1,0] op_sel_hi:[0,1]
	v_pk_fma_f32 v[34:35], v[50:51], v[34:35], v[66:67] op_sel_hi:[1,0,1]
	v_add_u32_e32 v50, 0x1000, v16
	v_ashrrev_i32_e32 v51, 31, v50
	v_lshl_add_u64 v[50:51], v[50:51], 3, s[46:47]
	v_mov_b32_e32 v50, v218
	v_mov_b32_e32 v51, v219
	v_xor_b32_e32 v66, 0x80000000, v37
	v_mov_b32_e32 v67, v37
	s_nop 0
	v_pk_mul_f32 v[66:67], v[66:67], v[50:51] op_sel:[0,1] op_sel_hi:[1,0]
	s_nop 0
	v_pk_fma_f32 v[36:37], v[36:37], v[50:51], v[66:67] op_sel_hi:[0,1,1]
	v_add_u32_e32 v50, 0x1200, v16
	v_ashrrev_i32_e32 v51, 31, v50
	v_lshl_add_u64 v[50:51], v[50:51], 3, s[46:47]
	v_mov_b32_e32 v50, v220
	v_mov_b32_e32 v51, v221
	v_xor_b32_e32 v66, 0x80000000, v41
	v_mov_b32_e32 v67, v41
	v_pk_add_f32 v[70:71], v[20:21], v[36:37]
	v_pk_add_f32 v[20:21], v[20:21], v[36:37] neg_lo:[0,1] neg_hi:[0,1]
	s_nop 0
	v_pk_mul_f32 v[66:67], v[66:67], v[50:51] op_sel:[0,1] op_sel_hi:[1,0]
	s_nop 0
	v_pk_fma_f32 v[40:41], v[40:41], v[50:51], v[66:67] op_sel_hi:[0,1,1]
	v_add_u32_e32 v50, 0x1400, v16
	v_ashrrev_i32_e32 v51, 31, v50
	v_lshl_add_u64 v[50:51], v[50:51], 3, s[46:47]
	v_mov_b32_e32 v50, v222
	v_mov_b32_e32 v51, v223
	v_xor_b32_e32 v66, 0x80000000, v43
	v_mov_b32_e32 v67, v43
	v_pk_add_f32 v[36:37], v[22:23], v[40:41]
	v_pk_add_f32 v[22:23], v[22:23], v[40:41] neg_lo:[0,1] neg_hi:[0,1]
	s_nop 0
	v_pk_mul_f32 v[66:67], v[66:67], v[50:51] op_sel:[0,1] op_sel_hi:[1,0]
	s_nop 0
	v_pk_fma_f32 v[42:43], v[42:43], v[50:51], v[66:67] op_sel_hi:[0,1,1]
	v_add_u32_e32 v50, 0x1600, v16
	v_ashrrev_i32_e32 v51, 31, v50
	v_lshl_add_u64 v[50:51], v[50:51], 3, s[46:47]
	v_mov_b32_e32 v50, v224
	v_mov_b32_e32 v51, v225
	v_xor_b32_e32 v66, 0x80000000, v47
	v_mov_b32_e32 v67, v47
	v_xor_b32_e32 v40, 0x80000000, v23
	v_mov_b32_e32 v41, v22
	s_nop 0
	v_pk_mul_f32 v[66:67], v[66:67], v[50:51] op_sel:[0,1] op_sel_hi:[1,0]
	s_nop 0
	v_pk_fma_f32 v[46:47], v[46:47], v[50:51], v[66:67] op_sel_hi:[0,1,1]
	v_add_u32_e32 v50, 0x1800, v16
	v_ashrrev_i32_e32 v51, 31, v50
	v_lshl_add_u64 v[50:51], v[50:51], 3, s[46:47]
	v_mov_b32_e32 v50, v226
	v_mov_b32_e32 v51, v227
	v_xor_b32_e32 v66, 0x80000000, v45
	v_mov_b32_e32 v67, v45
	s_nop 0
	v_pk_mul_f32 v[66:67], v[66:67], v[50:51] op_sel:[0,1] op_sel_hi:[1,0]
	s_nop 0
	v_pk_fma_f32 v[44:45], v[44:45], v[50:51], v[66:67] op_sel_hi:[0,1,1]
	v_add_u32_e32 v50, 0x1a00, v16
	v_ashrrev_i32_e32 v51, 31, v50
	v_lshl_add_u64 v[50:51], v[50:51], 3, s[46:47]
	v_mov_b32_e32 v50, v228
	v_mov_b32_e32 v51, v229
	v_xor_b32_e32 v66, 0x80000000, v49
	v_mov_b32_e32 v67, v49
	s_nop 0
	v_pk_mul_f32 v[66:67], v[66:67], v[50:51] op_sel:[0,1] op_sel_hi:[1,0]
	s_nop 0
	v_pk_fma_f32 v[48:49], v[48:49], v[50:51], v[66:67] op_sel_hi:[0,1,1]
	v_add_u32_e32 v50, 0x1c00, v16
	v_ashrrev_i32_e32 v51, 31, v50
	v_lshl_add_u64 v[50:51], v[50:51], 3, s[46:47]
	v_mov_b32_e32 v50, v230
	v_mov_b32_e32 v51, v231
	v_xor_b32_e32 v66, 0x80000000, v39
	v_mov_b32_e32 v67, v39
	s_nop 0
	v_pk_mul_f32 v[66:67], v[66:67], v[50:51] op_sel:[0,1] op_sel_hi:[1,0]
	s_nop 0
	v_pk_fma_f32 v[38:39], v[38:39], v[50:51], v[66:67] op_sel_hi:[0,1,1]
	v_add_u32_e32 v50, 0x1e00, v16
	v_ashrrev_i32_e32 v51, 31, v50
	v_lshl_add_u64 v[50:51], v[50:51], 3, s[46:47]
	v_mov_b32_e32 v50, v232
	v_mov_b32_e32 v51, v233
	v_lshlrev_b32_e32 v190, 3, v16
	v_add_u32_e32 v190, 0x11000, v190
	global_load_dwordx2 v[202:203], v190, s[46:47] offset:-4096
	global_load_dwordx2 v[204:205], v190, s[46:47]
	v_add_u32_e32 v190, 0x2000, v190
	global_load_dwordx2 v[206:207], v190, s[46:47] offset:-4096
	global_load_dwordx2 v[208:209], v190, s[46:47]
	v_add_u32_e32 v190, 0x2000, v190
	global_load_dwordx2 v[210:211], v190, s[46:47] offset:-4096
	global_load_dwordx2 v[212:213], v190, s[46:47]
	v_add_u32_e32 v190, 0x2000, v190
	global_load_dwordx2 v[214:215], v190, s[46:47] offset:-4096
	global_load_dwordx2 v[216:217], v190, s[46:47]
	v_add_u32_e32 v190, 0x2000, v190
	global_load_dwordx2 v[218:219], v190, s[46:47] offset:-4096
	global_load_dwordx2 v[220:221], v190, s[46:47]
	v_add_u32_e32 v190, 0x2000, v190
	global_load_dwordx2 v[222:223], v190, s[46:47] offset:-4096
	global_load_dwordx2 v[224:225], v190, s[46:47]
	v_add_u32_e32 v190, 0x2000, v190
	global_load_dwordx2 v[226:227], v190, s[46:47] offset:-4096
	global_load_dwordx2 v[228:229], v190, s[46:47]
	v_add_u32_e32 v190, 0x2000, v190
	global_load_dwordx2 v[230:231], v190, s[46:47] offset:-4096
	global_load_dwordx2 v[232:233], v190, s[46:47]
	v_xor_b32_e32 v66, 0x80000000, v19
	v_mov_b32_e32 v67, v19
	v_mov_b32_e32 v17, v164
	s_nop 0
	v_pk_mul_f32 v[66:67], v[66:67], v[50:51] op_sel:[0,1] op_sel_hi:[1,0]
	s_nop 0
	v_pk_fma_f32 v[18:19], v[18:19], v[50:51], v[66:67] op_sel_hi:[0,1,1]
	v_mov_b32_e32 v50, v165
	v_mov_b32_e32 v17, v166
	v_mov_b32_e32 v66, v167
	v_mov_b32_e32 v17, v168
	s_nop 0
	v_pk_mul_f32 v[40:41], v[40:41], v[68:69] op_sel_hi:[1,0]
	v_mov_b32_e32 v17, v170
	v_pk_fma_f32 v[22:23], v[22:23], v[50:51], v[40:41] op_sel_hi:[1,0,1]
	v_pk_add_f32 v[40:41], v[24:25], v[42:43]
	v_pk_add_f32 v[24:25], v[24:25], v[42:43] neg_lo:[0,1] neg_hi:[0,1]
	s_nop 0
	v_xor_b32_e32 v42, 0x80000000, v25
	v_mov_b32_e32 v43, v24
	v_pk_mul_f32 v[42:43], v[42:43], v[66:67] op_sel_hi:[1,0]
	v_mov_b32_e32 v17, v171
	v_pk_fma_f32 v[24:25], v[24:25], v[66:67], v[42:43] op_sel_hi:[1,0,1]
	v_pk_add_f32 v[42:43], v[26:27], v[46:47]
	v_pk_add_f32 v[26:27], v[26:27], v[46:47] neg_lo:[0,1] neg_hi:[0,1]
	s_nop 0
	v_pk_mul_f32 v[46:47], v[26:27], v[68:69] op_sel_hi:[1,0]
	v_xor_b32_e32 v72, 0x80000000, v27
	v_mov_b32_e32 v73, v26
	v_pk_fma_f32 v[26:27], v[72:73], v[50:51], v[46:47] op_sel_hi:[1,0,1]
	v_pk_add_f32 v[46:47], v[28:29], v[44:45]
	v_pk_add_f32 v[28:29], v[28:29], v[44:45] neg_lo:[0,1] neg_hi:[0,1]
	v_mov_b32_e32 v17, v175
	v_xor_b32_e32 v44, 0x80000000, v29
	v_mov_b32_e32 v45, v28
	v_pk_add_f32 v[28:29], v[30:31], v[48:49]
	v_pk_add_f32 v[30:31], v[30:31], v[48:49] neg_lo:[0,1] neg_hi:[0,1]
	s_nop 0
	v_pk_mul_f32 v[48:49], v[30:31], v[68:69] op_sel_hi:[1,0] neg_lo:[0,1] neg_hi:[0,1]
	v_xor_b32_e32 v72, 0x80000000, v31
	v_mov_b32_e32 v73, v30
	v_pk_fma_f32 v[30:31], v[72:73], v[50:51], v[48:49] op_sel_hi:[1,0,1]
	v_pk_add_f32 v[48:49], v[32:33], v[38:39]
	v_pk_add_f32 v[32:33], v[32:33], v[38:39] neg_lo:[0,1] neg_hi:[0,1]
	s_nop 0
	v_xor_b32_e32 v38, 0x80000000, v33
	v_mov_b32_e32 v39, v32
	v_pk_mul_f32 v[38:39], v[38:39], v[66:67] op_sel_hi:[1,0]
	s_nop 0
	v_pk_fma_f32 v[32:33], v[32:33], v[66:67], v[38:39] op_sel_hi:[1,0,1] neg_lo:[0,1,0] neg_hi:[0,1,0]
	v_pk_add_f32 v[38:39], v[34:35], v[18:19]
	v_pk_add_f32 v[18:19], v[34:35], v[18:19] neg_lo:[0,1] neg_hi:[0,1]
	s_nop 0
	v_xor_b32_e32 v34, 0x80000000, v19
	v_mov_b32_e32 v35, v18
	v_pk_mul_f32 v[34:35], v[34:35], v[68:69] op_sel_hi:[1,0]
	v_mov_b32_e32 v68, v169
	v_pk_fma_f32 v[18:19], v[18:19], v[50:51], v[34:35] op_sel_hi:[1,0,1] neg_lo:[0,1,0] neg_hi:[0,1,0]
	v_pk_add_f32 v[50:51], v[36:37], v[28:29]
	v_pk_add_f32 v[28:29], v[36:37], v[28:29] neg_lo:[0,1] neg_hi:[0,1]
	v_pk_add_f32 v[34:35], v[70:71], v[46:47]
	v_xor_b32_e32 v36, 0x80000000, v29
	v_mov_b32_e32 v37, v28
	v_pk_mul_f32 v[36:37], v[36:37], v[66:67] op_sel_hi:[1,0]
	v_pk_add_f32 v[46:47], v[70:71], v[46:47] neg_lo:[0,1] neg_hi:[0,1]
	v_pk_fma_f32 v[28:29], v[28:29], v[66:67], v[36:37] op_sel_hi:[1,0,1]
	v_pk_add_f32 v[36:37], v[40:41], v[48:49]
	v_pk_add_f32 v[40:41], v[40:41], v[48:49] neg_lo:[0,1] neg_hi:[0,1]
	s_nop 0
	v_xor_b32_e32 v48, 0x80000000, v41
	v_mov_b32_e32 v49, v40
	v_pk_add_f32 v[40:41], v[42:43], v[38:39]
	v_pk_add_f32 v[38:39], v[42:43], v[38:39] neg_lo:[0,1] neg_hi:[0,1]
	s_nop 0
	v_xor_b32_e32 v42, 0x80000000, v39
	v_mov_b32_e32 v43, v38
	v_pk_mul_f32 v[42:43], v[66:67], v[42:43] op_sel_hi:[0,1]
	v_pk_fma_f32 v[38:39], v[38:39], v[66:67], v[42:43] op_sel_hi:[1,0,1] neg_lo:[0,1,0] neg_hi:[0,1,0]
	v_pk_add_f32 v[42:43], v[34:35], v[36:37]
	v_pk_add_f32 v[34:35], v[34:35], v[36:37] neg_lo:[0,1] neg_hi:[0,1]
	v_pk_add_f32 v[36:37], v[50:51], v[40:41]
	v_pk_add_f32 v[40:41], v[50:51], v[40:41] neg_lo:[0,1] neg_hi:[0,1]
	s_nop 0
	v_xor_b32_e32 v50, 0x80000000, v41
	v_mov_b32_e32 v51, v40
	v_pk_add_f32 v[40:41], v[42:43], v[36:37]
	v_pk_add_f32 v[36:37], v[42:43], v[36:37] neg_lo:[0,1] neg_hi:[0,1]
	v_pk_add_f32 v[42:43], v[34:35], v[50:51]
	v_pk_add_f32 v[34:35], v[34:35], v[50:51] neg_lo:[0,1] neg_hi:[0,1]
	v_pk_add_f32 v[50:51], v[46:47], v[48:49]
	v_pk_add_f32 v[46:47], v[46:47], v[48:49] neg_lo:[0,1] neg_hi:[0,1]
	v_pk_add_f32 v[48:49], v[28:29], v[38:39]
	v_pk_add_f32 v[28:29], v[28:29], v[38:39] neg_lo:[0,1] neg_hi:[0,1]
	s_nop 0
	v_xor_b32_e32 v38, 0x80000000, v29
	v_mov_b32_e32 v39, v28
	v_pk_add_f32 v[28:29], v[50:51], v[48:49]
	v_pk_add_f32 v[48:49], v[50:51], v[48:49] neg_lo:[0,1] neg_hi:[0,1]
	v_pk_add_f32 v[50:51], v[46:47], v[38:39]
	v_pk_add_f32 v[38:39], v[46:47], v[38:39] neg_lo:[0,1] neg_hi:[0,1]
	v_pk_add_f32 v[46:47], v[20:21], v[44:45]
	v_pk_add_f32 v[20:21], v[20:21], v[44:45] neg_lo:[0,1] neg_hi:[0,1]
	v_pk_add_f32 v[44:45], v[22:23], v[30:31]
	v_pk_add_f32 v[22:23], v[22:23], v[30:31] neg_lo:[0,1] neg_hi:[0,1]
	s_nop 0
	v_xor_b32_e32 v30, 0x80000000, v23
	v_mov_b32_e32 v31, v22
	v_pk_mul_f32 v[30:31], v[66:67], v[30:31] op_sel_hi:[0,1]
	v_pk_fma_f32 v[22:23], v[66:67], v[22:23], v[30:31] op_sel_hi:[0,1,1]
	v_pk_add_f32 v[30:31], v[24:25], v[32:33]
	v_pk_add_f32 v[24:25], v[24:25], v[32:33] neg_lo:[0,1] neg_hi:[0,1]
	s_nop 0
	v_xor_b32_e32 v32, 0x80000000, v25
	v_mov_b32_e32 v33, v24
	v_pk_add_f32 v[24:25], v[26:27], v[18:19]
	v_pk_add_f32 v[18:19], v[26:27], v[18:19] neg_lo:[0,1] neg_hi:[0,1]
	s_nop 0
	v_xor_b32_e32 v26, 0x80000000, v19
	v_mov_b32_e32 v27, v18
	v_pk_mul_f32 v[26:27], v[66:67], v[26:27] op_sel_hi:[0,1]
	v_pk_fma_f32 v[18:19], v[66:67], v[18:19], v[26:27] op_sel_hi:[0,1,1] neg_lo:[1,0,0] neg_hi:[1,0,0]
	v_pk_add_f32 v[26:27], v[46:47], v[30:31]
	v_pk_add_f32 v[30:31], v[46:47], v[30:31] neg_lo:[0,1] neg_hi:[0,1]
	v_pk_add_f32 v[46:47], v[44:45], v[24:25]
	v_pk_add_f32 v[24:25], v[44:45], v[24:25] neg_lo:[0,1] neg_hi:[0,1]
	v_mov_b32_e32 v66, v167
	v_xor_b32_e32 v44, 0x80000000, v25
	v_mov_b32_e32 v45, v24
	v_pk_add_f32 v[24:25], v[26:27], v[46:47]
	v_pk_add_f32 v[26:27], v[26:27], v[46:47] neg_lo:[0,1] neg_hi:[0,1]
	v_pk_add_f32 v[46:47], v[30:31], v[44:45]
	v_pk_add_f32 v[30:31], v[30:31], v[44:45] neg_lo:[0,1] neg_hi:[0,1]
	v_pk_add_f32 v[44:45], v[20:21], v[32:33]
	v_pk_add_f32 v[20:21], v[20:21], v[32:33] neg_lo:[0,1] neg_hi:[0,1]
	v_pk_add_f32 v[32:33], v[22:23], v[18:19]
	v_pk_add_f32 v[18:19], v[22:23], v[18:19] neg_lo:[0,1] neg_hi:[0,1]
	s_nop 0
	v_xor_b32_e32 v22, 0x80000000, v19
	v_mov_b32_e32 v23, v18
	v_pk_add_f32 v[18:19], v[44:45], v[32:33]
	v_pk_add_f32 v[32:33], v[44:45], v[32:33] neg_lo:[0,1] neg_hi:[0,1]
	v_pk_add_f32 v[44:45], v[20:21], v[22:23]
	v_pk_add_f32 v[20:21], v[20:21], v[22:23] neg_lo:[0,1] neg_hi:[0,1]
	ds_write_b64 v10, v[40:41]
	ds_write_b64 v13, v[24:25]
	ds_write_b64 v15, v[28:29]
	ds_write_b64 v52, v[18:19]
	ds_write_b64 v53, v[42:43]
	ds_write_b64 v54, v[46:47]
	ds_write_b64 v55, v[50:51]
	ds_write_b64 v56, v[44:45]
	ds_write_b64 v57, v[36:37]
	ds_write_b64 v58, v[26:27]
	ds_write_b64 v59, v[48:49]
	ds_write_b64 v60, v[32:33]
	ds_write_b64 v61, v[34:35]
	ds_write_b64 v62, v[30:31]
	ds_write_b64 v63, v[38:39]
	ds_write_b64 v64, v[20:21]
	v_mov_b32_e32 v10, v177
	v_mov_b32_e32 v64, v165
	v_lshlrev_b32_e32 v13, 3, v17
	v_lshlrev_b32_e32 v48, 3, v10
	v_add3_u32 v10, 0, v13, v48
	v_xor_b32_e32 v13, 1, v17
	v_xor_b32_e32 v34, 8, v17
	v_xor_b32_e32 v36, 9, v17
	v_lshlrev_b32_e32 v13, 3, v13
	v_xor_b32_e32 v15, 2, v17
	v_xor_b32_e32 v24, 3, v17
	v_xor_b32_e32 v26, 4, v17
	v_xor_b32_e32 v28, 5, v17
	v_xor_b32_e32 v30, 6, v17
	v_xor_b32_e32 v32, 7, v17
	v_lshlrev_b32_e32 v34, 3, v34
	v_lshlrev_b32_e32 v36, 3, v36
	v_xor_b32_e32 v38, 10, v17
	v_xor_b32_e32 v40, 11, v17
	v_xor_b32_e32 v42, 12, v17
	v_xor_b32_e32 v44, 13, v17
	v_xor_b32_e32 v46, 14, v17
	v_xor_b32_e32 v17, 15, v17
	v_add3_u32 v13, 0, v13, v48
	v_lshlrev_b32_e32 v15, 3, v15
	v_lshlrev_b32_e32 v24, 3, v24
	v_lshlrev_b32_e32 v26, 3, v26
	v_lshlrev_b32_e32 v28, 3, v28
	v_lshlrev_b32_e32 v30, 3, v30
	v_lshlrev_b32_e32 v32, 3, v32
	v_add3_u32 v55, 0, v34, v48
	v_add3_u32 v56, 0, v36, v48
	v_lshlrev_b32_e32 v38, 3, v38
	v_lshlrev_b32_e32 v40, 3, v40
	v_lshlrev_b32_e32 v42, 3, v42
	v_lshlrev_b32_e32 v44, 3, v44
	v_lshlrev_b32_e32 v46, 3, v46
	v_lshlrev_b32_e32 v17, 3, v17
	ds_read_b64 v[18:19], v10
	ds_read_b64 v[20:21], v13
	v_add3_u32 v15, 0, v15, v48
	v_add3_u32 v50, 0, v24, v48
	v_add3_u32 v51, 0, v26, v48
	v_add3_u32 v52, 0, v28, v48
	v_add3_u32 v53, 0, v30, v48
	v_add3_u32 v54, 0, v32, v48
	ds_read_b64 v[34:35], v55
	ds_read_b64 v[36:37], v56
	v_add3_u32 v57, 0, v38, v48
	v_add3_u32 v58, 0, v40, v48
	v_add3_u32 v59, 0, v42, v48
	v_add3_u32 v60, 0, v44, v48
	v_add3_u32 v61, 0, v46, v48
	v_add3_u32 v62, 0, v17, v48
	v_mov_b32_e32 v17, v1
	ds_read_b64 v[22:23], v15
	ds_read_b64 v[24:25], v50
	ds_read_b64 v[26:27], v51
	ds_read_b64 v[28:29], v52
	ds_read_b64 v[30:31], v53
	ds_read_b64 v[32:33], v54
	ds_read_b64 v[38:39], v57
	ds_read_b64 v[40:41], v58
	ds_read_b64 v[42:43], v59
	ds_read_b64 v[44:45], v60
	ds_read_b64 v[46:47], v61
	ds_read_b64 v[48:49], v62
	s_waitcnt lgkmcnt(13)
	v_pk_add_f32 v[70:71], v[18:19], v[34:35]
	v_mov_b32_e32 v17, v164
	v_pk_add_f32 v[18:19], v[18:19], v[34:35] neg_lo:[0,1] neg_hi:[0,1]
	v_mov_b32_e32 v17, v166
	s_waitcnt lgkmcnt(12)
	v_pk_add_f32 v[34:35], v[20:21], v[36:37]
	v_pk_add_f32 v[20:21], v[20:21], v[36:37] neg_lo:[0,1] neg_hi:[0,1]
	v_mov_b32_e32 v17, v168
	v_xor_b32_e32 v36, 0x80000000, v21
	v_mov_b32_e32 v37, v20
	s_nop 0
	v_pk_mul_f32 v[36:37], v[36:37], v[68:69] op_sel_hi:[1,0] neg_lo:[0,1] neg_hi:[0,1]
	v_mov_b32_e32 v17, v170
	v_pk_fma_f32 v[20:21], v[20:21], v[64:65], v[36:37] op_sel_hi:[1,0,1]
	s_waitcnt lgkmcnt(5)
	v_pk_add_f32 v[36:37], v[22:23], v[38:39]
	v_pk_add_f32 v[22:23], v[22:23], v[38:39] neg_lo:[0,1] neg_hi:[0,1]
	s_nop 0
	v_xor_b32_e32 v38, 0x80000000, v23
	v_mov_b32_e32 v39, v22
	v_pk_mul_f32 v[38:39], v[38:39], v[66:67] op_sel_hi:[1,0] neg_lo:[0,1] neg_hi:[0,1]
	v_mov_b32_e32 v17, v171
	v_pk_fma_f32 v[22:23], v[22:23], v[66:67], v[38:39] op_sel_hi:[1,0,1]
	s_waitcnt lgkmcnt(4)
	v_pk_add_f32 v[38:39], v[24:25], v[40:41]
	v_pk_add_f32 v[24:25], v[24:25], v[40:41] neg_lo:[0,1] neg_hi:[0,1]
	s_nop 0
	v_pk_mul_f32 v[40:41], v[24:25], v[68:69] op_sel_hi:[1,0]
	v_xor_b32_e32 v72, 0x80000000, v25
	v_mov_b32_e32 v73, v24
	v_pk_fma_f32 v[24:25], v[72:73], v[64:65], v[40:41] op_sel_hi:[1,0,1] neg_lo:[0,1,0] neg_hi:[0,1,0]
	s_waitcnt lgkmcnt(3)
	v_pk_add_f32 v[40:41], v[26:27], v[42:43]
	v_pk_add_f32 v[26:27], v[26:27], v[42:43] neg_lo:[0,1] neg_hi:[0,1]
	s_nop 0
	v_xor_b32_e32 v73, 0x80000000, v26
	v_mov_b32_e32 v72, v27
	s_waitcnt lgkmcnt(2)
	v_pk_add_f32 v[26:27], v[28:29], v[44:45]
	v_pk_add_f32 v[28:29], v[28:29], v[44:45] neg_lo:[0,1] neg_hi:[0,1]
	s_nop 0
	v_pk_mul_f32 v[42:43], v[28:29], v[68:69] op_sel_hi:[1,0] neg_lo:[0,1] neg_hi:[0,1]
	v_xor_b32_e32 v44, 0x80000000, v29
	v_mov_b32_e32 v45, v28
	v_pk_fma_f32 v[28:29], v[44:45], v[64:65], v[42:43] op_sel_hi:[1,0,1] neg_lo:[0,1,0] neg_hi:[0,1,0]
	s_waitcnt lgkmcnt(1)
	v_pk_add_f32 v[42:43], v[30:31], v[46:47]
	v_pk_add_f32 v[30:31], v[30:31], v[46:47] neg_lo:[0,1] neg_hi:[0,1]
	s_nop 0
	v_xor_b32_e32 v44, 0x80000000, v31
	v_mov_b32_e32 v45, v30
	v_pk_mul_f32 v[44:45], v[44:45], v[66:67] op_sel_hi:[1,0] neg_lo:[0,1] neg_hi:[0,1]
	s_nop 0
	v_pk_fma_f32 v[30:31], v[30:31], v[66:67], v[44:45] op_sel_hi:[1,0,1] neg_lo:[0,1,0] neg_hi:[0,1,0]
	s_waitcnt lgkmcnt(0)
	v_pk_add_f32 v[44:45], v[32:33], v[48:49]
	v_pk_add_f32 v[32:33], v[32:33], v[48:49] neg_lo:[0,1] neg_hi:[0,1]
	v_pk_add_f32 v[48:49], v[34:35], v[26:27]
	v_pk_add_f32 v[26:27], v[34:35], v[26:27] neg_lo:[0,1] neg_hi:[0,1]
	v_xor_b32_e32 v46, 0x80000000, v33
	v_xor_b32_e32 v34, 0x80000000, v27
	v_mov_b32_e32 v35, v26
	v_pk_mul_f32 v[34:35], v[34:35], v[66:67] op_sel_hi:[1,0] neg_lo:[0,1] neg_hi:[0,1]
	v_mov_b32_e32 v47, v32
	v_pk_fma_f32 v[26:27], v[26:27], v[66:67], v[34:35] op_sel_hi:[1,0,1]
	v_pk_add_f32 v[34:35], v[36:37], v[42:43]
	v_pk_add_f32 v[36:37], v[36:37], v[42:43] neg_lo:[0,1] neg_hi:[0,1]
	v_pk_mul_f32 v[46:47], v[46:47], v[68:69] op_sel_hi:[1,0] neg_lo:[0,1] neg_hi:[0,1]
	v_xor_b32_e32 v43, 0x80000000, v36
	v_mov_b32_e32 v42, v37
	v_pk_add_f32 v[36:37], v[38:39], v[44:45]
	v_pk_add_f32 v[38:39], v[38:39], v[44:45] neg_lo:[0,1] neg_hi:[0,1]
	v_pk_fma_f32 v[46:47], v[32:33], v[64:65], v[46:47] op_sel_hi:[1,0,1] neg_lo:[0,1,0] neg_hi:[0,1,0]
	v_xor_b32_e32 v44, 0x80000000, v39
	v_mov_b32_e32 v45, v38
	v_pk_add_f32 v[32:33], v[70:71], v[40:41]
	v_pk_mul_f32 v[44:45], v[44:45], v[66:67] op_sel_hi:[1,0] neg_lo:[0,1] neg_hi:[0,1]
	v_pk_add_f32 v[40:41], v[70:71], v[40:41] neg_lo:[0,1] neg_hi:[0,1]
	v_pk_fma_f32 v[38:39], v[38:39], v[66:67], v[44:45] op_sel_hi:[1,0,1] neg_lo:[0,1,0] neg_hi:[0,1,0]
	v_pk_add_f32 v[44:45], v[32:33], v[34:35]
	v_pk_add_f32 v[32:33], v[32:33], v[34:35] neg_lo:[0,1] neg_hi:[0,1]
	v_pk_add_f32 v[34:35], v[48:49], v[36:37]
	v_pk_add_f32 v[36:37], v[48:49], v[36:37] neg_lo:[0,1] neg_hi:[0,1]
	v_pk_add_f32 v[64:65], v[44:45], v[34:35]
	v_xor_b32_e32 v49, 0x80000000, v36
	v_mov_b32_e32 v48, v37
	v_pk_add_f32 v[36:37], v[44:45], v[34:35] neg_lo:[0,1] neg_hi:[0,1]
	v_pk_add_f32 v[68:69], v[32:33], v[48:49]
	v_pk_add_f32 v[44:45], v[32:33], v[48:49] neg_lo:[0,1] neg_hi:[0,1]
	v_pk_add_f32 v[32:33], v[40:41], v[42:43]
	v_pk_add_f32 v[34:35], v[40:41], v[42:43] neg_lo:[0,1] neg_hi:[0,1]
	v_pk_add_f32 v[40:41], v[26:27], v[38:39]
	v_pk_add_f32 v[26:27], v[26:27], v[38:39] neg_lo:[0,1] neg_hi:[0,1]
	v_pk_add_f32 v[42:43], v[32:33], v[40:41] neg_lo:[0,1] neg_hi:[0,1]
	v_xor_b32_e32 v39, 0x80000000, v26
	v_mov_b32_e32 v38, v27
	v_pk_add_f32 v[26:27], v[32:33], v[40:41]
	v_pk_add_f32 v[40:41], v[20:21], v[28:29]
	v_pk_add_f32 v[20:21], v[20:21], v[28:29] neg_lo:[0,1] neg_hi:[0,1]
	v_pk_add_f32 v[32:33], v[34:35], v[38:39]
	v_xor_b32_e32 v28, 0x80000000, v21
	v_mov_b32_e32 v29, v20
	v_pk_mul_f32 v[28:29], v[66:67], v[28:29] op_sel_hi:[0,1] neg_lo:[1,0] neg_hi:[1,0]
	v_pk_fma_f32 v[20:21], v[66:67], v[20:21], v[28:29] op_sel_hi:[0,1,1]
	v_pk_add_f32 v[28:29], v[22:23], v[30:31]
	v_pk_add_f32 v[22:23], v[22:23], v[30:31] neg_lo:[0,1] neg_hi:[0,1]
	v_pk_add_f32 v[38:39], v[34:35], v[38:39] neg_lo:[0,1] neg_hi:[0,1]
	v_xor_b32_e32 v31, 0x80000000, v22
	v_mov_b32_e32 v30, v23
	v_pk_add_f32 v[22:23], v[24:25], v[46:47]
	v_pk_add_f32 v[24:25], v[24:25], v[46:47] neg_lo:[0,1] neg_hi:[0,1]
	v_pk_add_f32 v[34:35], v[18:19], v[72:73]
	v_xor_b32_e32 v46, 0x80000000, v25
	v_mov_b32_e32 v47, v24
	v_pk_mul_f32 v[46:47], v[66:67], v[46:47] op_sel_hi:[0,1] neg_lo:[1,0] neg_hi:[1,0]
	v_pk_fma_f32 v[24:25], v[66:67], v[24:25], v[46:47] op_sel_hi:[0,1,1] neg_lo:[1,0,0] neg_hi:[1,0,0]
	v_pk_add_f32 v[46:47], v[34:35], v[28:29]
	v_pk_add_f32 v[28:29], v[34:35], v[28:29] neg_lo:[0,1] neg_hi:[0,1]
	v_pk_add_f32 v[34:35], v[40:41], v[22:23]
	v_pk_add_f32 v[22:23], v[40:41], v[22:23] neg_lo:[0,1] neg_hi:[0,1]
	v_pk_add_f32 v[18:19], v[18:19], v[72:73] neg_lo:[0,1] neg_hi:[0,1]
	v_xor_b32_e32 v49, 0x80000000, v22
	v_mov_b32_e32 v48, v23
	v_pk_add_f32 v[66:67], v[28:29], v[48:49]
	v_pk_add_f32 v[48:49], v[28:29], v[48:49] neg_lo:[0,1] neg_hi:[0,1]
	v_pk_add_f32 v[28:29], v[18:19], v[30:31]
	v_pk_add_f32 v[18:19], v[18:19], v[30:31] neg_lo:[0,1] neg_hi:[0,1]
	v_pk_add_f32 v[30:31], v[20:21], v[24:25]
	v_pk_add_f32 v[20:21], v[20:21], v[24:25] neg_lo:[0,1] neg_hi:[0,1]
	v_pk_add_f32 v[22:23], v[46:47], v[34:35]
	v_xor_b32_e32 v25, 0x80000000, v20
	v_add_u32_e32 v20, 0x2000, v16
	v_mov_b32_e32 v24, v21
	v_ashrrev_i32_e32 v21, 31, v20
	v_lshl_add_u64 v[20:21], v[20:21], 3, s[46:47]
	s_waitcnt vmcnt(0)
	v_mov_b32_e32 v20, v202
	v_mov_b32_e32 v21, v203
	v_pk_add_f32 v[40:41], v[46:47], v[34:35] neg_lo:[0,1] neg_hi:[0,1]
	v_pk_add_f32 v[34:35], v[18:19], v[24:25]
	v_pk_add_f32 v[18:19], v[18:19], v[24:25] neg_lo:[0,1] neg_hi:[0,1]
	v_xor_b32_e32 v24, 0x80000000, v65
	v_mov_b32_e32 v25, v65
	v_pk_add_f32 v[70:71], v[28:29], v[30:31]
	v_pk_add_f32 v[46:47], v[28:29], v[30:31] neg_lo:[0,1] neg_hi:[0,1]
	v_xor_b32_e32 v28, 0x80000000, v23
	v_mov_b32_e32 v29, v23
	v_xor_b32_e32 v30, 0x80000000, v69
	v_mov_b32_e32 v31, v69
	s_nop 0
	v_pk_mul_f32 v[24:25], v[24:25], v[20:21] op_sel:[0,1] op_sel_hi:[1,0]
	s_nop 0
	v_pk_fma_f32 v[20:21], v[64:65], v[20:21], v[24:25] op_sel_hi:[0,1,1]
	v_add_u32_e32 v24, 0x2200, v16
	v_ashrrev_i32_e32 v25, 31, v24
	v_lshl_add_u64 v[24:25], v[24:25], 3, s[46:47]
	v_mov_b32_e32 v24, v204
	v_mov_b32_e32 v25, v205
	v_xor_b32_e32 v64, 0x80000000, v67
	v_mov_b32_e32 v65, v67
	s_nop 0
	v_pk_mul_f32 v[28:29], v[24:25], v[28:29] op_sel:[1,0] op_sel_hi:[0,1]
	v_pk_fma_f32 v[22:23], v[24:25], v[22:23], v[28:29] op_sel_hi:[1,0,1]
	v_add_u32_e32 v24, 0x2400, v16
	v_ashrrev_i32_e32 v25, 31, v24
	v_lshl_add_u64 v[24:25], v[24:25], 3, s[46:47]
	v_mov_b32_e32 v24, v206
	v_mov_b32_e32 v25, v207
	v_xor_b32_e32 v28, 0x80000000, v27
	v_mov_b32_e32 v29, v27
	s_nop 0
	v_pk_mul_f32 v[28:29], v[28:29], v[24:25] op_sel:[0,1] op_sel_hi:[1,0]
	s_nop 0
	v_pk_fma_f32 v[24:25], v[26:27], v[24:25], v[28:29] op_sel_hi:[0,1,1]
	v_add_u32_e32 v26, 0x2600, v16
	v_ashrrev_i32_e32 v27, 31, v26
	v_lshl_add_u64 v[26:27], v[26:27], 3, s[46:47]
	v_mov_b32_e32 v26, v208
	v_mov_b32_e32 v27, v209
	v_xor_b32_e32 v28, 0x80000000, v71
	v_mov_b32_e32 v29, v71
	s_nop 0
	v_pk_mul_f32 v[28:29], v[26:27], v[28:29] op_sel:[1,0] op_sel_hi:[0,1]
	v_pk_fma_f32 v[26:27], v[26:27], v[70:71], v[28:29] op_sel_hi:[1,0,1]
	v_add_u32_e32 v28, 0x2800, v16
	v_ashrrev_i32_e32 v29, 31, v28
	v_lshl_add_u64 v[28:29], v[28:29], 3, s[46:47]
	v_mov_b32_e32 v28, v210
	v_mov_b32_e32 v29, v211
	s_nop 0
	v_pk_mul_f32 v[30:31], v[30:31], v[28:29] op_sel:[0,1] op_sel_hi:[1,0]
	s_nop 0
	v_pk_fma_f32 v[28:29], v[68:69], v[28:29], v[30:31] op_sel_hi:[0,1,1]
	v_add_u32_e32 v30, 0x2a00, v16
	v_ashrrev_i32_e32 v31, 31, v30
	v_lshl_add_u64 v[30:31], v[30:31], 3, s[46:47]
	v_mov_b32_e32 v30, v212
	v_mov_b32_e32 v31, v213
	s_nop 0
	v_pk_mul_f32 v[64:65], v[30:31], v[64:65] op_sel:[1,0] op_sel_hi:[0,1]
	v_pk_fma_f32 v[30:31], v[30:31], v[66:67], v[64:65] op_sel_hi:[1,0,1]
	v_add_u32_e32 v64, 0x2c00, v16
	v_ashrrev_i32_e32 v65, 31, v64
	v_lshl_add_u64 v[64:65], v[64:65], 3, s[46:47]
	v_mov_b32_e32 v64, v214
	v_mov_b32_e32 v65, v215
	v_xor_b32_e32 v66, 0x80000000, v33
	v_mov_b32_e32 v67, v33
	s_nop 0
	v_pk_mul_f32 v[66:67], v[66:67], v[64:65] op_sel:[0,1] op_sel_hi:[1,0]
	s_nop 0
	v_pk_fma_f32 v[32:33], v[32:33], v[64:65], v[66:67] op_sel_hi:[0,1,1]
	v_add_u32_e32 v64, 0x2e00, v16
	v_ashrrev_i32_e32 v65, 31, v64
	v_lshl_add_u64 v[64:65], v[64:65], 3, s[46:47]
	v_mov_b32_e32 v64, v216
	v_mov_b32_e32 v65, v217
	v_xor_b32_e32 v66, 0x80000000, v35
	v_mov_b32_e32 v67, v35
	s_nop 0
	v_pk_mul_f32 v[66:67], v[64:65], v[66:67] op_sel:[1,0] op_sel_hi:[0,1]
	v_pk_fma_f32 v[34:35], v[64:65], v[34:35], v[66:67] op_sel_hi:[1,0,1]
	v_add_u32_e32 v64, 0x3000, v16
	v_ashrrev_i32_e32 v65, 31, v64
	v_lshl_add_u64 v[64:65], v[64:65], 3, s[46:47]
	v_mov_b32_e32 v64, v218
	v_mov_b32_e32 v65, v219
	v_xor_b32_e32 v66, 0x80000000, v37
	v_mov_b32_e32 v67, v37
	s_nop 0
	v_pk_mul_f32 v[66:67], v[66:67], v[64:65] op_sel:[0,1] op_sel_hi:[1,0]
	s_nop 0
	v_pk_fma_f32 v[36:37], v[36:37], v[64:65], v[66:67] op_sel_hi:[0,1,1]
	v_add_u32_e32 v64, 0x3200, v16
	v_ashrrev_i32_e32 v65, 31, v64
	v_lshl_add_u64 v[64:65], v[64:65], 3, s[46:47]
	v_mov_b32_e32 v64, v220
	v_mov_b32_e32 v65, v221
	v_xor_b32_e32 v66, 0x80000000, v41
	v_mov_b32_e32 v67, v41
	v_pk_add_f32 v[68:69], v[20:21], v[36:37]
	v_pk_add_f32 v[20:21], v[20:21], v[36:37] neg_lo:[0,1] neg_hi:[0,1]
	s_nop 0
	v_pk_mul_f32 v[66:67], v[66:67], v[64:65] op_sel:[0,1] op_sel_hi:[1,0]
	s_nop 0
	v_pk_fma_f32 v[40:41], v[40:41], v[64:65], v[66:67] op_sel_hi:[0,1,1]
	v_add_u32_e32 v64, 0x3400, v16
	v_ashrrev_i32_e32 v65, 31, v64
	v_lshl_add_u64 v[64:65], v[64:65], 3, s[46:47]
	v_mov_b32_e32 v64, v222
	v_mov_b32_e32 v65, v223
	v_xor_b32_e32 v66, 0x80000000, v43
	v_mov_b32_e32 v67, v43
	v_pk_add_f32 v[36:37], v[22:23], v[40:41]
	v_pk_add_f32 v[22:23], v[22:23], v[40:41] neg_lo:[0,1] neg_hi:[0,1]
	s_nop 0
	v_pk_mul_f32 v[66:67], v[66:67], v[64:65] op_sel:[0,1] op_sel_hi:[1,0]
	s_nop 0
	v_pk_fma_f32 v[42:43], v[42:43], v[64:65], v[66:67] op_sel_hi:[0,1,1]
	v_add_u32_e32 v64, 0x3600, v16
	v_ashrrev_i32_e32 v65, 31, v64
	v_lshl_add_u64 v[64:65], v[64:65], 3, s[46:47]
	v_mov_b32_e32 v64, v224
	v_mov_b32_e32 v65, v225
	v_xor_b32_e32 v66, 0x80000000, v47
	v_mov_b32_e32 v67, v47
	v_xor_b32_e32 v40, 0x80000000, v23
	v_mov_b32_e32 v41, v22
	s_nop 0
	v_pk_mul_f32 v[66:67], v[66:67], v[64:65] op_sel:[0,1] op_sel_hi:[1,0]
	s_nop 0
	v_pk_fma_f32 v[46:47], v[46:47], v[64:65], v[66:67] op_sel_hi:[0,1,1]
	v_add_u32_e32 v64, 0x3800, v16
	v_ashrrev_i32_e32 v65, 31, v64
	v_lshl_add_u64 v[64:65], v[64:65], 3, s[46:47]
	v_mov_b32_e32 v64, v226
	v_mov_b32_e32 v65, v227
	v_xor_b32_e32 v66, 0x80000000, v45
	v_mov_b32_e32 v67, v45
	s_nop 0
	v_pk_mul_f32 v[66:67], v[66:67], v[64:65] op_sel:[0,1] op_sel_hi:[1,0]
	s_nop 0
	v_pk_fma_f32 v[44:45], v[44:45], v[64:65], v[66:67] op_sel_hi:[0,1,1]
	v_add_u32_e32 v64, 0x3a00, v16
	v_ashrrev_i32_e32 v65, 31, v64
	v_lshl_add_u64 v[64:65], v[64:65], 3, s[46:47]
	v_mov_b32_e32 v64, v228
	v_mov_b32_e32 v65, v229
	v_xor_b32_e32 v66, 0x80000000, v49
	v_mov_b32_e32 v67, v49
	s_nop 0
	v_pk_mul_f32 v[66:67], v[66:67], v[64:65] op_sel:[0,1] op_sel_hi:[1,0]
	s_nop 0
	v_pk_fma_f32 v[48:49], v[48:49], v[64:65], v[66:67] op_sel_hi:[0,1,1]
	v_add_u32_e32 v64, 0x3c00, v16
	v_ashrrev_i32_e32 v65, 31, v64
	v_lshl_add_u64 v[64:65], v[64:65], 3, s[46:47]
	v_add_u32_e32 v16, 0x3e00, v16
	v_mov_b32_e32 v64, v230
	v_mov_b32_e32 v65, v231
	v_ashrrev_i32_e32 v17, 31, v16
	v_lshl_add_u64 v[16:17], v[16:17], 3, s[46:47]
	v_mov_b32_e32 v16, v232
	v_mov_b32_e32 v17, v233
	v_xor_b32_e32 v66, 0x80000000, v39
	v_mov_b32_e32 v67, v39
	s_nop 0
	v_pk_mul_f32 v[66:67], v[66:67], v[64:65] op_sel:[0,1] op_sel_hi:[1,0]
	s_nop 0
	v_pk_fma_f32 v[38:39], v[38:39], v[64:65], v[66:67] op_sel_hi:[0,1,1]
	v_xor_b32_e32 v64, 0x80000000, v19
	v_mov_b32_e32 v65, v19
	s_nop 0
	v_pk_mul_f32 v[64:65], v[64:65], v[16:17] op_sel:[0,1] op_sel_hi:[1,0]
	v_mov_b32_e32 v66, v169
	v_pk_fma_f32 v[16:17], v[18:19], v[16:17], v[64:65] op_sel_hi:[0,1,1]
	v_mov_b32_e32 v18, v1
	v_mov_b32_e32 v19, v166
	v_mov_b32_e32 v18, v164
	v_mov_b32_e32 v64, v167
	v_mov_b32_e32 v18, v165
	s_nop 0
	v_mov_b32_e32 v19, v168
	s_nop 0
	v_mov_b32_e32 v19, v170
	v_pk_mul_f32 v[40:41], v[40:41], v[66:67] op_sel_hi:[1,0]
	v_mov_b32_e32 v19, v171
	s_nop 0
	v_pk_fma_f32 v[22:23], v[22:23], v[18:19], v[40:41] op_sel_hi:[1,0,1]
	v_pk_add_f32 v[40:41], v[24:25], v[42:43]
	v_pk_add_f32 v[24:25], v[24:25], v[42:43] neg_lo:[0,1] neg_hi:[0,1]
	s_nop 0
	v_xor_b32_e32 v42, 0x80000000, v25
	v_mov_b32_e32 v43, v24
	v_pk_mul_f32 v[42:43], v[42:43], v[64:65] op_sel_hi:[1,0]
	s_nop 0
	v_pk_fma_f32 v[24:25], v[24:25], v[64:65], v[42:43] op_sel_hi:[1,0,1]
	v_pk_add_f32 v[42:43], v[26:27], v[46:47]
	v_pk_add_f32 v[26:27], v[26:27], v[46:47] neg_lo:[0,1] neg_hi:[0,1]
	s_nop 0
	v_pk_mul_f32 v[46:47], v[26:27], v[66:67] op_sel_hi:[1,0]
	v_xor_b32_e32 v70, 0x80000000, v27
	v_mov_b32_e32 v71, v26
	v_pk_fma_f32 v[26:27], v[70:71], v[18:19], v[46:47] op_sel_hi:[1,0,1]
	v_pk_add_f32 v[46:47], v[28:29], v[44:45]
	v_pk_add_f32 v[28:29], v[28:29], v[44:45] neg_lo:[0,1] neg_hi:[0,1]
	s_nop 0
	v_xor_b32_e32 v44, 0x80000000, v29
	v_mov_b32_e32 v45, v28
	v_pk_add_f32 v[28:29], v[30:31], v[48:49]
	v_pk_add_f32 v[30:31], v[30:31], v[48:49] neg_lo:[0,1] neg_hi:[0,1]
	s_nop 0
	v_pk_mul_f32 v[48:49], v[30:31], v[66:67] op_sel_hi:[1,0] neg_lo:[0,1] neg_hi:[0,1]
	v_xor_b32_e32 v70, 0x80000000, v31
	v_mov_b32_e32 v71, v30
	v_pk_fma_f32 v[30:31], v[70:71], v[18:19], v[48:49] op_sel_hi:[1,0,1]
	v_pk_add_f32 v[48:49], v[32:33], v[38:39]
	v_pk_add_f32 v[32:33], v[32:33], v[38:39] neg_lo:[0,1] neg_hi:[0,1]
	s_nop 0
	v_xor_b32_e32 v38, 0x80000000, v33
	v_mov_b32_e32 v39, v32
	v_pk_mul_f32 v[38:39], v[38:39], v[64:65] op_sel_hi:[1,0]
	s_nop 0
	v_pk_fma_f32 v[32:33], v[32:33], v[64:65], v[38:39] op_sel_hi:[1,0,1] neg_lo:[0,1,0] neg_hi:[0,1,0]
	v_pk_add_f32 v[38:39], v[34:35], v[16:17]
	v_pk_add_f32 v[16:17], v[34:35], v[16:17] neg_lo:[0,1] neg_hi:[0,1]
	s_nop 0
	v_xor_b32_e32 v34, 0x80000000, v17
	v_mov_b32_e32 v35, v16
	v_pk_mul_f32 v[34:35], v[34:35], v[66:67] op_sel_hi:[1,0]
	s_nop 0
	v_pk_fma_f32 v[16:17], v[16:17], v[18:19], v[34:35] op_sel_hi:[1,0,1] neg_lo:[0,1,0] neg_hi:[0,1,0]
	v_pk_add_f32 v[18:19], v[68:69], v[46:47]
	v_pk_add_f32 v[34:35], v[68:69], v[46:47] neg_lo:[0,1] neg_hi:[0,1]
	v_pk_add_f32 v[46:47], v[36:37], v[28:29]
	v_pk_add_f32 v[28:29], v[36:37], v[28:29] neg_lo:[0,1] neg_hi:[0,1]
	s_nop 0
	v_xor_b32_e32 v36, 0x80000000, v29
	v_mov_b32_e32 v37, v28
	v_pk_mul_f32 v[36:37], v[36:37], v[64:65] op_sel_hi:[1,0]
	s_nop 0
	v_pk_fma_f32 v[28:29], v[28:29], v[64:65], v[36:37] op_sel_hi:[1,0,1]
	v_pk_add_f32 v[36:37], v[40:41], v[48:49]
	v_pk_add_f32 v[40:41], v[40:41], v[48:49] neg_lo:[0,1] neg_hi:[0,1]
	s_nop 0
	v_xor_b32_e32 v48, 0x80000000, v41
	v_mov_b32_e32 v49, v40
	v_pk_add_f32 v[40:41], v[42:43], v[38:39]
	v_pk_add_f32 v[38:39], v[42:43], v[38:39] neg_lo:[0,1] neg_hi:[0,1]
	s_nop 0
	v_xor_b32_e32 v42, 0x80000000, v39
	v_mov_b32_e32 v43, v38
	v_pk_mul_f32 v[42:43], v[64:65], v[42:43] op_sel_hi:[0,1]
	v_pk_fma_f32 v[38:39], v[38:39], v[64:65], v[42:43] op_sel_hi:[1,0,1] neg_lo:[0,1,0] neg_hi:[0,1,0]
	v_pk_add_f32 v[42:43], v[18:19], v[36:37]
	v_pk_add_f32 v[18:19], v[18:19], v[36:37] neg_lo:[0,1] neg_hi:[0,1]
	v_pk_add_f32 v[36:37], v[46:47], v[40:41]
	v_pk_add_f32 v[40:41], v[46:47], v[40:41] neg_lo:[0,1] neg_hi:[0,1]
	s_nop 0
	v_xor_b32_e32 v46, 0x80000000, v41
	v_mov_b32_e32 v47, v40
	v_pk_add_f32 v[40:41], v[42:43], v[36:37]
	v_pk_add_f32 v[36:37], v[42:43], v[36:37] neg_lo:[0,1] neg_hi:[0,1]
	v_pk_add_f32 v[42:43], v[18:19], v[46:47]
	v_pk_add_f32 v[18:19], v[18:19], v[46:47] neg_lo:[0,1] neg_hi:[0,1]
	v_pk_add_f32 v[46:47], v[34:35], v[48:49]
	v_pk_add_f32 v[34:35], v[34:35], v[48:49] neg_lo:[0,1] neg_hi:[0,1]
	v_pk_add_f32 v[48:49], v[28:29], v[38:39]
	v_pk_add_f32 v[28:29], v[28:29], v[38:39] neg_lo:[0,1] neg_hi:[0,1]
	s_nop 0
	v_xor_b32_e32 v38, 0x80000000, v29
	v_mov_b32_e32 v39, v28
	v_pk_add_f32 v[28:29], v[46:47], v[48:49]
	v_pk_add_f32 v[46:47], v[46:47], v[48:49] neg_lo:[0,1] neg_hi:[0,1]
	v_pk_add_f32 v[48:49], v[34:35], v[38:39]
	v_pk_add_f32 v[34:35], v[34:35], v[38:39] neg_lo:[0,1] neg_hi:[0,1]
	v_pk_add_f32 v[38:39], v[20:21], v[44:45]
	v_pk_add_f32 v[20:21], v[20:21], v[44:45] neg_lo:[0,1] neg_hi:[0,1]
	v_pk_add_f32 v[44:45], v[22:23], v[30:31]
	v_pk_add_f32 v[22:23], v[22:23], v[30:31] neg_lo:[0,1] neg_hi:[0,1]
	s_nop 0
	v_xor_b32_e32 v30, 0x80000000, v23
	v_mov_b32_e32 v31, v22
	v_pk_mul_f32 v[30:31], v[64:65], v[30:31] op_sel_hi:[0,1]
	v_pk_fma_f32 v[22:23], v[64:65], v[22:23], v[30:31] op_sel_hi:[0,1,1]
	v_pk_add_f32 v[30:31], v[24:25], v[32:33]
	v_pk_add_f32 v[24:25], v[24:25], v[32:33] neg_lo:[0,1] neg_hi:[0,1]
	s_nop 0
	v_xor_b32_e32 v32, 0x80000000, v25
	v_mov_b32_e32 v33, v24
	v_pk_add_f32 v[24:25], v[26:27], v[16:17]
	v_pk_add_f32 v[16:17], v[26:27], v[16:17] neg_lo:[0,1] neg_hi:[0,1]
	s_nop 0
	v_xor_b32_e32 v26, 0x80000000, v17
	v_mov_b32_e32 v27, v16
	v_pk_mul_f32 v[26:27], v[64:65], v[26:27] op_sel_hi:[0,1]
	v_pk_fma_f32 v[16:17], v[64:65], v[16:17], v[26:27] op_sel_hi:[0,1,1] neg_lo:[1,0,0] neg_hi:[1,0,0]
	v_pk_add_f32 v[26:27], v[38:39], v[30:31]
	v_pk_add_f32 v[30:31], v[38:39], v[30:31] neg_lo:[0,1] neg_hi:[0,1]
	v_pk_add_f32 v[38:39], v[44:45], v[24:25]
	v_pk_add_f32 v[24:25], v[44:45], v[24:25] neg_lo:[0,1] neg_hi:[0,1]
	s_nop 0
	v_xor_b32_e32 v44, 0x80000000, v25
	v_mov_b32_e32 v45, v24
	v_pk_add_f32 v[24:25], v[26:27], v[38:39]
	v_pk_add_f32 v[26:27], v[26:27], v[38:39] neg_lo:[0,1] neg_hi:[0,1]
	v_pk_add_f32 v[38:39], v[30:31], v[44:45]
	v_pk_add_f32 v[30:31], v[30:31], v[44:45] neg_lo:[0,1] neg_hi:[0,1]
	v_pk_add_f32 v[44:45], v[20:21], v[32:33]
	v_pk_add_f32 v[20:21], v[20:21], v[32:33] neg_lo:[0,1] neg_hi:[0,1]
	v_pk_add_f32 v[32:33], v[22:23], v[16:17]
	v_pk_add_f32 v[16:17], v[22:23], v[16:17] neg_lo:[0,1] neg_hi:[0,1]
	s_nop 0
	v_xor_b32_e32 v22, 0x80000000, v17
	v_mov_b32_e32 v23, v16
	v_pk_add_f32 v[16:17], v[44:45], v[32:33]
	v_pk_add_f32 v[32:33], v[44:45], v[32:33] neg_lo:[0,1] neg_hi:[0,1]
	v_pk_add_f32 v[44:45], v[20:21], v[22:23]
	v_pk_add_f32 v[20:21], v[20:21], v[22:23] neg_lo:[0,1] neg_hi:[0,1]
	ds_write_b64 v10, v[40:41]
	ds_write_b64 v13, v[24:25]
	ds_write_b64 v15, v[28:29]
	ds_write_b64 v50, v[16:17]
	ds_write_b64 v51, v[42:43]
	ds_write_b64 v52, v[38:39]
	ds_write_b64 v53, v[48:49]
	ds_write_b64 v54, v[44:45]
	ds_write_b64 v55, v[36:37]
	ds_write_b64 v56, v[26:27]
	ds_write_b64 v57, v[46:47]
	ds_write_b64 v58, v[32:33]
	ds_write_b64 v59, v[18:19]
	ds_write_b64 v60, v[30:31]
	ds_write_b64 v61, v[34:35]
	ds_write_b64 v62, v[20:21]
	v_mov_b32_e32 v10, v174
	v_mov_b32_e32 v50, v172
	s_waitcnt lgkmcnt(0)
	s_barrier
	v_mov_b32_e32 v20, v180
	v_add_u32_e32 v13, v50, v10
	v_mov_b32_e32 v21, v181
	v_lshl_add_u32 v13, v13, 3, 0
	ds_read2_b64 v[16:19], v13 offset1:16
	v_xad_u32 v15, v50, 1, v10
	v_lshl_add_u32 v15, v15, 3, 0
	s_waitcnt lgkmcnt(0)
	v_xor_b32_e32 v23, 0x80000000, v16
	v_mov_b32_e32 v22, v17
	v_pk_fma_f32 v[16:17], v[22:23], 0, v[16:17] op_sel_hi:[1,0,1]
	v_pk_fma_f32 v[22:23], v[20:21], s[90:91], v[20:21] op_sel:[1,0,0] op_sel_hi:[0,1,1]
	v_xor_b32_e32 v25, 0x80000000, v18
	v_mov_b32_e32 v24, v19
	v_pk_mul_f32 v[24:25], v[22:23], v[24:25] op_sel:[1,0]
	s_nop 0
	v_pk_fma_f32 v[18:19], v[18:19], v[22:23], v[24:25] op_sel_hi:[1,0,1]
	v_xor_b32_e32 v24, 0x80000000, v23
	v_mov_b32_e32 v25, v23
	v_pk_mul_f32 v[24:25], v[20:21], v[24:25] op_sel:[1,0] op_sel_hi:[0,1]
	v_pk_fma_f32 v[26:27], v[20:21], v[22:23], v[24:25] op_sel_hi:[1,0,1]
	ds_read2_b64 v[22:25], v15 offset0:32 offset1:48
	s_waitcnt lgkmcnt(0)
	v_xor_b32_e32 v29, 0x80000000, v22
	v_mov_b32_e32 v28, v23
	v_pk_mul_f32 v[28:29], v[28:29], v[26:27] op_sel:[0,1]
	s_nop 0
	v_pk_fma_f32 v[22:23], v[22:23], v[26:27], v[28:29] op_sel_hi:[1,0,1]
	v_xor_b32_e32 v28, 0x80000000, v27
	v_mov_b32_e32 v29, v27
	v_pk_mul_f32 v[28:29], v[20:21], v[28:29] op_sel:[1,0] op_sel_hi:[0,1]
	v_pk_fma_f32 v[26:27], v[20:21], v[26:27], v[28:29] op_sel_hi:[1,0,1]
	v_xor_b32_e32 v29, 0x80000000, v24
	v_mov_b32_e32 v28, v25
	v_pk_mul_f32 v[28:29], v[28:29], v[26:27] op_sel:[0,1]
	s_nop 0
	v_pk_fma_f32 v[24:25], v[24:25], v[26:27], v[28:29] op_sel_hi:[1,0,1]
	v_xor_b32_e32 v28, 0x80000000, v27
	v_mov_b32_e32 v29, v27
	v_pk_mul_f32 v[28:29], v[20:21], v[28:29] op_sel:[1,0] op_sel_hi:[0,1]
	v_pk_fma_f32 v[26:27], v[20:21], v[26:27], v[28:29] op_sel_hi:[1,0,1]
	v_xad_u32 v28, v50, 2, v10
	v_lshl_add_u32 v51, v28, 3, 0
	ds_read2_b64 v[28:31], v51 offset0:64 offset1:80
	v_xor_b32_e32 v32, 0x80000000, v27
	v_mov_b32_e32 v33, v27
	v_pk_mul_f32 v[32:33], v[20:21], v[32:33] op_sel:[1,0] op_sel_hi:[0,1]
	s_waitcnt lgkmcnt(0)
	v_xor_b32_e32 v35, 0x80000000, v28
	v_mov_b32_e32 v34, v29
	v_pk_mul_f32 v[34:35], v[34:35], v[26:27] op_sel:[0,1]
	s_nop 0
	v_pk_fma_f32 v[28:29], v[28:29], v[26:27], v[34:35] op_sel_hi:[1,0,1]
	v_pk_fma_f32 v[34:35], v[20:21], v[26:27], v[32:33] op_sel_hi:[1,0,1]
	v_xor_b32_e32 v27, 0x80000000, v30
	v_mov_b32_e32 v26, v31
	v_pk_mul_f32 v[26:27], v[26:27], v[34:35] op_sel:[0,1]
	v_xor_b32_e32 v36, 0x80000000, v35
	v_pk_fma_f32 v[26:27], v[30:31], v[34:35], v[26:27] op_sel_hi:[1,0,1]
	v_xad_u32 v30, v50, 3, v10
	v_lshl_add_u32 v54, v30, 3, 0
	ds_read2_b64 v[30:33], v54 offset0:96 offset1:112
	v_mov_b32_e32 v37, v35
	v_pk_mul_f32 v[36:37], v[20:21], v[36:37] op_sel:[1,0] op_sel_hi:[0,1]
	v_pk_fma_f32 v[34:35], v[20:21], v[34:35], v[36:37] op_sel_hi:[1,0,1]
	s_waitcnt lgkmcnt(0)
	v_xor_b32_e32 v37, 0x80000000, v30
	v_mov_b32_e32 v36, v31
	v_pk_mul_f32 v[36:37], v[36:37], v[34:35] op_sel:[0,1]
	s_nop 0
	v_pk_fma_f32 v[30:31], v[30:31], v[34:35], v[36:37] op_sel_hi:[1,0,1]
	v_xor_b32_e32 v36, 0x80000000, v35
	v_mov_b32_e32 v37, v35
	v_pk_mul_f32 v[36:37], v[20:21], v[36:37] op_sel:[1,0] op_sel_hi:[0,1]
	v_pk_fma_f32 v[34:35], v[20:21], v[34:35], v[36:37] op_sel_hi:[1,0,1]
	v_xor_b32_e32 v37, 0x80000000, v32
	v_mov_b32_e32 v36, v33
	v_pk_mul_f32 v[36:37], v[36:37], v[34:35] op_sel:[0,1]
	s_nop 0
	v_pk_fma_f32 v[32:33], v[32:33], v[34:35], v[36:37] op_sel_hi:[1,0,1]
	v_xor_b32_e32 v36, 0x80000000, v35
	v_mov_b32_e32 v37, v35
	v_pk_mul_f32 v[36:37], v[20:21], v[36:37] op_sel:[1,0] op_sel_hi:[0,1]
	v_pk_fma_f32 v[38:39], v[20:21], v[34:35], v[36:37] op_sel_hi:[1,0,1]
	v_xad_u32 v34, v50, 4, v10
	v_lshl_add_u32 v55, v34, 3, 0
	ds_read2_b64 v[34:37], v55 offset0:128 offset1:144
	v_xor_b32_e32 v40, 0x80000000, v39
	v_mov_b32_e32 v41, v39
	v_pk_mul_f32 v[40:41], v[20:21], v[40:41] op_sel:[1,0] op_sel_hi:[0,1]
	s_waitcnt lgkmcnt(0)
	v_xor_b32_e32 v43, 0x80000000, v34
	v_mov_b32_e32 v42, v35
	v_pk_mul_f32 v[42:43], v[42:43], v[38:39] op_sel:[0,1]
	s_nop 0
	v_pk_fma_f32 v[34:35], v[34:35], v[38:39], v[42:43] op_sel_hi:[1,0,1]
	v_pk_fma_f32 v[42:43], v[20:21], v[38:39], v[40:41] op_sel_hi:[1,0,1]
	v_xor_b32_e32 v39, 0x80000000, v36
	v_mov_b32_e32 v38, v37
	v_pk_mul_f32 v[38:39], v[38:39], v[42:43] op_sel:[0,1]
	v_xor_b32_e32 v44, 0x80000000, v43
	v_pk_fma_f32 v[36:37], v[36:37], v[42:43], v[38:39] op_sel_hi:[1,0,1]
	v_xad_u32 v38, v50, 5, v10
	v_lshl_add_u32 v56, v38, 3, 0
	ds_read2_b64 v[38:41], v56 offset0:160 offset1:176
	v_mov_b32_e32 v45, v43
	v_pk_mul_f32 v[44:45], v[20:21], v[44:45] op_sel:[1,0] op_sel_hi:[0,1]
	v_pk_fma_f32 v[42:43], v[20:21], v[42:43], v[44:45] op_sel_hi:[1,0,1]
	s_waitcnt lgkmcnt(0)
	v_xor_b32_e32 v45, 0x80000000, v38
	v_mov_b32_e32 v44, v39
	v_pk_mul_f32 v[44:45], v[44:45], v[42:43] op_sel:[0,1]
	s_nop 0
	v_pk_fma_f32 v[38:39], v[38:39], v[42:43], v[44:45] op_sel_hi:[1,0,1]
	v_xor_b32_e32 v44, 0x80000000, v43
	v_mov_b32_e32 v45, v43
	v_pk_mul_f32 v[44:45], v[20:21], v[44:45] op_sel:[1,0] op_sel_hi:[0,1]
	v_pk_fma_f32 v[42:43], v[20:21], v[42:43], v[44:45] op_sel_hi:[1,0,1]
	v_xor_b32_e32 v45, 0x80000000, v40
	v_mov_b32_e32 v44, v41
	v_pk_mul_f32 v[44:45], v[44:45], v[42:43] op_sel:[0,1]
	s_nop 0
	v_pk_fma_f32 v[40:41], v[40:41], v[42:43], v[44:45] op_sel_hi:[1,0,1]
	v_xor_b32_e32 v44, 0x80000000, v43
	v_mov_b32_e32 v45, v43
	v_pk_mul_f32 v[44:45], v[20:21], v[44:45] op_sel:[1,0] op_sel_hi:[0,1]
	v_pk_fma_f32 v[42:43], v[20:21], v[42:43], v[44:45] op_sel_hi:[1,0,1]
	v_xad_u32 v44, v50, 6, v10
	v_lshl_add_u32 v57, v44, 3, 0
	ds_read2_b64 v[44:47], v57 offset0:192 offset1:208
	v_xor_b32_e32 v48, 0x80000000, v43
	v_mov_b32_e32 v49, v43
	v_pk_mul_f32 v[48:49], v[20:21], v[48:49] op_sel:[1,0] op_sel_hi:[0,1]
	s_waitcnt lgkmcnt(0)
	v_xor_b32_e32 v53, 0x80000000, v44
	v_mov_b32_e32 v52, v45
	v_pk_mul_f32 v[52:53], v[52:53], v[42:43] op_sel:[0,1]
	s_nop 0
	v_pk_fma_f32 v[44:45], v[44:45], v[42:43], v[52:53] op_sel_hi:[1,0,1]
	v_pk_fma_f32 v[52:53], v[20:21], v[42:43], v[48:49] op_sel_hi:[1,0,1]
	v_xor_b32_e32 v43, 0x80000000, v46
	v_mov_b32_e32 v42, v47
	v_pk_mul_f32 v[42:43], v[42:43], v[52:53] op_sel:[0,1]
	v_xor_b32_e32 v60, 0x80000000, v53
	v_pk_fma_f32 v[42:43], v[46:47], v[52:53], v[42:43] op_sel_hi:[1,0,1]
	v_xad_u32 v46, v50, 7, v10
	v_lshl_add_u32 v58, v46, 3, 0
	ds_read2_b64 v[46:49], v58 offset0:224 offset1:240
	v_mov_b32_e32 v61, v53
	v_pk_mul_f32 v[60:61], v[20:21], v[60:61] op_sel:[1,0] op_sel_hi:[0,1]
	v_pk_fma_f32 v[52:53], v[20:21], v[52:53], v[60:61] op_sel_hi:[1,0,1]
	s_waitcnt lgkmcnt(0)
	v_xor_b32_e32 v61, 0x80000000, v46
	v_mov_b32_e32 v60, v47
	v_pk_mul_f32 v[60:61], v[60:61], v[52:53] op_sel:[0,1]
	s_nop 0
	v_pk_fma_f32 v[46:47], v[46:47], v[52:53], v[60:61] op_sel_hi:[1,0,1]
	v_xor_b32_e32 v60, 0x80000000, v53
	v_mov_b32_e32 v61, v53
	v_pk_mul_f32 v[60:61], v[20:21], v[60:61] op_sel:[1,0] op_sel_hi:[0,1]
	v_pk_fma_f32 v[52:53], v[20:21], v[52:53], v[60:61] op_sel_hi:[1,0,1]
	v_xor_b32_e32 v61, 0x80000000, v48
	v_mov_b32_e32 v60, v49
	v_pk_mul_f32 v[60:61], v[60:61], v[52:53] op_sel:[0,1]
	s_nop 0
	v_pk_fma_f32 v[48:49], v[48:49], v[52:53], v[60:61] op_sel_hi:[1,0,1]
	v_xor_b32_e32 v60, 0x80000000, v53
	v_mov_b32_e32 v61, v53
	v_pk_mul_f32 v[60:61], v[20:21], v[60:61] op_sel:[1,0] op_sel_hi:[0,1]
	v_pk_fma_f32 v[64:65], v[20:21], v[52:53], v[60:61] op_sel_hi:[1,0,1]
	v_xad_u32 v52, v50, 8, v10
	v_lshl_add_u32 v52, v52, 3, 0
	v_add_u32_e32 v59, 0x800, v52
	ds_read2_b64 v[60:63], v59 offset1:16
	v_xor_b32_e32 v52, 0x80000000, v65
	v_mov_b32_e32 v53, v65
	v_pk_mul_f32 v[66:67], v[20:21], v[52:53] op_sel:[1,0] op_sel_hi:[0,1]
	v_pk_fma_f32 v[66:67], v[20:21], v[64:65], v[66:67] op_sel_hi:[1,0,1]
	s_waitcnt lgkmcnt(0)
	v_xor_b32_e32 v53, 0x80000000, v60
	v_mov_b32_e32 v52, v61
	v_pk_mul_f32 v[52:53], v[52:53], v[64:65] op_sel:[0,1]
	v_xor_b32_e32 v68, 0x80000000, v67
	v_pk_fma_f32 v[52:53], v[60:61], v[64:65], v[52:53] op_sel_hi:[1,0,1]
	v_xor_b32_e32 v61, 0x80000000, v62
	v_mov_b32_e32 v60, v63
	v_pk_mul_f32 v[60:61], v[60:61], v[66:67] op_sel:[0,1]
	v_mov_b32_e32 v69, v67
	v_pk_fma_f32 v[70:71], v[62:63], v[66:67], v[60:61] op_sel_hi:[1,0,1]
	v_xad_u32 v60, v50, 9, v10
	v_lshl_add_u32 v60, v60, 3, 0
	v_add_u32_e32 v60, 0x800, v60
	ds_read2_b64 v[62:65], v60 offset0:32 offset1:48
	v_pk_mul_f32 v[68:69], v[20:21], v[68:69] op_sel:[1,0] op_sel_hi:[0,1]
	v_pk_fma_f32 v[66:67], v[20:21], v[66:67], v[68:69] op_sel_hi:[1,0,1]
	s_waitcnt lgkmcnt(0)
	v_xor_b32_e32 v69, 0x80000000, v62
	v_mov_b32_e32 v68, v63
	v_pk_mul_f32 v[68:69], v[68:69], v[66:67] op_sel:[0,1]
	s_nop 0
	v_pk_fma_f32 v[72:73], v[62:63], v[66:67], v[68:69] op_sel_hi:[1,0,1]
	v_xor_b32_e32 v62, 0x80000000, v67
	v_mov_b32_e32 v63, v67
	v_pk_mul_f32 v[62:63], v[20:21], v[62:63] op_sel:[1,0] op_sel_hi:[0,1]
	v_pk_fma_f32 v[62:63], v[20:21], v[66:67], v[62:63] op_sel_hi:[1,0,1]
	v_xor_b32_e32 v67, 0x80000000, v64
	v_mov_b32_e32 v66, v65
	v_pk_mul_f32 v[66:67], v[66:67], v[62:63] op_sel:[0,1]
	s_nop 0
	v_pk_fma_f32 v[74:75], v[64:65], v[62:63], v[66:67] op_sel_hi:[1,0,1]
	v_xor_b32_e32 v64, 0x80000000, v63
	v_mov_b32_e32 v65, v63
	v_pk_mul_f32 v[64:65], v[20:21], v[64:65] op_sel:[1,0] op_sel_hi:[0,1]
	v_pk_fma_f32 v[66:67], v[20:21], v[62:63], v[64:65] op_sel_hi:[1,0,1]
	v_xad_u32 v61, v50, 10, v10
	v_lshl_add_u32 v61, v61, 3, 0
	v_add_u32_e32 v61, 0x800, v61
	ds_read2_b64 v[62:65], v61 offset0:64 offset1:80
	v_xor_b32_e32 v68, 0x80000000, v67
	v_mov_b32_e32 v69, v67
	v_pk_mul_f32 v[68:69], v[20:21], v[68:69] op_sel:[1,0] op_sel_hi:[0,1]
	v_pk_fma_f32 v[68:69], v[20:21], v[66:67], v[68:69] op_sel_hi:[1,0,1]
	s_waitcnt lgkmcnt(0)
	v_xor_b32_e32 v77, 0x80000000, v62
	v_mov_b32_e32 v76, v63
	v_pk_mul_f32 v[76:77], v[76:77], v[66:67] op_sel:[0,1]
	v_xor_b32_e32 v80, 0x80000000, v69
	v_pk_fma_f32 v[76:77], v[62:63], v[66:67], v[76:77] op_sel_hi:[1,0,1]
	v_xor_b32_e32 v63, 0x80000000, v64
	v_mov_b32_e32 v62, v65
	v_pk_mul_f32 v[62:63], v[62:63], v[68:69] op_sel:[0,1]
	v_mov_b32_e32 v81, v69
	v_pk_fma_f32 v[78:79], v[64:65], v[68:69], v[62:63] op_sel_hi:[1,0,1]
	v_xad_u32 v62, v50, 11, v10
	v_lshl_add_u32 v62, v62, 3, 0
	v_add_u32_e32 v62, 0x800, v62
	ds_read2_b64 v[64:67], v62 offset0:96 offset1:112
	v_pk_mul_f32 v[80:81], v[20:21], v[80:81] op_sel:[1,0] op_sel_hi:[0,1]
	v_pk_fma_f32 v[68:69], v[20:21], v[68:69], v[80:81] op_sel_hi:[1,0,1]
	s_waitcnt lgkmcnt(0)
	v_xor_b32_e32 v81, 0x80000000, v64
	v_mov_b32_e32 v80, v65
	v_pk_mul_f32 v[80:81], v[80:81], v[68:69] op_sel:[0,1]
	s_nop 0
	v_pk_fma_f32 v[80:81], v[64:65], v[68:69], v[80:81] op_sel_hi:[1,0,1]
	v_xor_b32_e32 v64, 0x80000000, v69
	v_mov_b32_e32 v65, v69
	v_pk_mul_f32 v[64:65], v[20:21], v[64:65] op_sel:[1,0] op_sel_hi:[0,1]
	v_pk_fma_f32 v[64:65], v[20:21], v[68:69], v[64:65] op_sel_hi:[1,0,1]
	v_xor_b32_e32 v69, 0x80000000, v66
	v_mov_b32_e32 v68, v67
	v_pk_mul_f32 v[68:69], v[68:69], v[64:65] op_sel:[0,1]
	s_nop 0
	v_pk_fma_f32 v[82:83], v[66:67], v[64:65], v[68:69] op_sel_hi:[1,0,1]
	v_xor_b32_e32 v66, 0x80000000, v65
	v_mov_b32_e32 v67, v65
	v_pk_mul_f32 v[66:67], v[20:21], v[66:67] op_sel:[1,0] op_sel_hi:[0,1]
	v_pk_fma_f32 v[68:69], v[20:21], v[64:65], v[66:67] op_sel_hi:[1,0,1]
	v_xad_u32 v63, v50, 12, v10
	v_lshl_add_u32 v63, v63, 3, 0
	v_add_u32_e32 v63, 0x800, v63
	ds_read2_b64 v[64:67], v63 offset0:128 offset1:144
	v_xor_b32_e32 v84, 0x80000000, v69
	v_mov_b32_e32 v85, v69
	v_pk_mul_f32 v[84:85], v[20:21], v[84:85] op_sel:[1,0] op_sel_hi:[0,1]
	v_pk_fma_f32 v[84:85], v[20:21], v[68:69], v[84:85] op_sel_hi:[1,0,1]
	s_waitcnt lgkmcnt(0)
	v_xor_b32_e32 v87, 0x80000000, v64
	v_mov_b32_e32 v86, v65
	v_pk_mul_f32 v[86:87], v[86:87], v[68:69] op_sel:[0,1]
	v_xor_b32_e32 v90, 0x80000000, v85
	v_pk_fma_f32 v[86:87], v[64:65], v[68:69], v[86:87] op_sel_hi:[1,0,1]
	v_xor_b32_e32 v65, 0x80000000, v66
	v_mov_b32_e32 v64, v67
	v_pk_mul_f32 v[64:65], v[64:65], v[84:85] op_sel:[0,1]
	v_mov_b32_e32 v91, v85
	v_pk_fma_f32 v[88:89], v[66:67], v[84:85], v[64:65] op_sel_hi:[1,0,1]
	v_xad_u32 v64, v50, 13, v10
	v_lshl_add_u32 v64, v64, 3, 0
	v_add_u32_e32 v64, 0x800, v64
	ds_read2_b64 v[66:69], v64 offset0:160 offset1:176
	v_pk_mul_f32 v[90:91], v[20:21], v[90:91] op_sel:[1,0] op_sel_hi:[0,1]
	v_pk_fma_f32 v[84:85], v[20:21], v[84:85], v[90:91] op_sel_hi:[1,0,1]
	s_waitcnt lgkmcnt(0)
	v_xor_b32_e32 v91, 0x80000000, v66
	v_mov_b32_e32 v90, v67
	v_pk_mul_f32 v[90:91], v[90:91], v[84:85] op_sel:[0,1]
	s_nop 0
	v_pk_fma_f32 v[90:91], v[66:67], v[84:85], v[90:91] op_sel_hi:[1,0,1]
	v_xor_b32_e32 v66, 0x80000000, v85
	v_mov_b32_e32 v67, v85
	v_pk_mul_f32 v[66:67], v[20:21], v[66:67] op_sel:[1,0] op_sel_hi:[0,1]
	v_pk_fma_f32 v[66:67], v[20:21], v[84:85], v[66:67] op_sel_hi:[1,0,1]
	v_xor_b32_e32 v85, 0x80000000, v68
	v_mov_b32_e32 v84, v69
	v_pk_mul_f32 v[84:85], v[84:85], v[66:67] op_sel:[0,1]
	s_nop 0
	v_pk_fma_f32 v[84:85], v[68:69], v[66:67], v[84:85] op_sel_hi:[1,0,1]
	v_xor_b32_e32 v68, 0x80000000, v67
	v_mov_b32_e32 v69, v67
	v_pk_mul_f32 v[68:69], v[20:21], v[68:69] op_sel:[1,0] op_sel_hi:[0,1]
	v_pk_fma_f32 v[92:93], v[20:21], v[66:67], v[68:69] op_sel_hi:[1,0,1]
	v_xad_u32 v65, v50, 14, v10
	v_lshl_add_u32 v65, v65, 3, 0
	v_add_u32_e32 v65, 0x800, v65
	ds_read2_b64 v[66:69], v65 offset0:192 offset1:208
	v_xor_b32_e32 v94, 0x80000000, v93
	v_mov_b32_e32 v95, v93
	v_pk_mul_f32 v[94:95], v[20:21], v[94:95] op_sel:[1,0] op_sel_hi:[0,1]
	v_xad_u32 v10, v50, 15, v10
	s_waitcnt lgkmcnt(0)
	v_xor_b32_e32 v97, 0x80000000, v66
	v_mov_b32_e32 v96, v67
	v_pk_mul_f32 v[96:97], v[96:97], v[92:93] op_sel:[0,1]
	v_lshl_add_u32 v10, v10, 3, 0
	v_pk_fma_f32 v[96:97], v[66:67], v[92:93], v[96:97] op_sel_hi:[1,0,1]
	v_pk_fma_f32 v[92:93], v[20:21], v[92:93], v[94:95] op_sel_hi:[1,0,1]
	v_xor_b32_e32 v67, 0x80000000, v68
	v_mov_b32_e32 v66, v69
	v_pk_mul_f32 v[66:67], v[66:67], v[92:93] op_sel:[0,1]
	v_add_u32_e32 v101, 0x800, v10
	v_pk_fma_f32 v[94:95], v[68:69], v[92:93], v[66:67] op_sel_hi:[1,0,1]
	ds_read2_b64 v[66:69], v101 offset0:224 offset1:240
	v_xor_b32_e32 v98, 0x80000000, v93
	v_mov_b32_e32 v99, v93
	v_pk_mul_f32 v[98:99], v[20:21], v[98:99] op_sel:[1,0] op_sel_hi:[0,1]
	v_pk_fma_f32 v[92:93], v[20:21], v[92:93], v[98:99] op_sel_hi:[1,0,1]
	s_waitcnt lgkmcnt(0)
	v_xor_b32_e32 v99, 0x80000000, v66
	v_mov_b32_e32 v98, v67
	v_pk_mul_f32 v[98:99], v[98:99], v[92:93] op_sel:[0,1]
	s_nop 0
	v_pk_fma_f32 v[66:67], v[66:67], v[92:93], v[98:99] op_sel_hi:[1,0,1]
	v_xor_b32_e32 v98, 0x80000000, v93
	v_mov_b32_e32 v99, v93
	v_pk_mul_f32 v[98:99], v[20:21], v[98:99] op_sel:[1,0] op_sel_hi:[0,1]
	v_pk_fma_f32 v[20:21], v[20:21], v[92:93], v[98:99] op_sel_hi:[1,0,1]
	v_xor_b32_e32 v93, 0x80000000, v68
	v_mov_b32_e32 v92, v69
	v_pk_mul_f32 v[92:93], v[92:93], v[20:21] op_sel:[0,1]
	s_nop 0
	v_pk_fma_f32 v[68:69], v[68:69], v[20:21], v[92:93] op_sel_hi:[1,0,1]
	v_mov_b32_e32 v10, v1
	v_pk_add_f32 v[104:105], v[16:17], v[52:53]
	v_pk_add_f32 v[16:17], v[16:17], v[52:53] neg_lo:[0,1] neg_hi:[0,1]
	v_pk_add_f32 v[52:53], v[18:19], v[70:71]
	v_pk_add_f32 v[18:19], v[18:19], v[70:71] neg_lo:[0,1] neg_hi:[0,1]
	v_mov_b32_e32 v92, v164
	v_mov_b32_e32 v20, v165
	v_mov_b32_e32 v98, v166
	v_mov_b32_e32 v10, v167
	v_mov_b32_e32 v100, v168
	v_mov_b32_e32 v50, v169
	v_mov_b32_e32 v102, v170
	v_xor_b32_e32 v70, 0x80000000, v19
	v_mov_b32_e32 v71, v18
	v_mov_b32_e32 v21, v171
	v_pk_mul_f32 v[70:71], v[102:103], v[70:71] op_sel_hi:[0,1]
	v_pk_fma_f32 v[18:19], v[92:93], v[18:19], v[70:71] op_sel_hi:[0,1,1]
	v_pk_add_f32 v[70:71], v[22:23], v[72:73]
	v_pk_add_f32 v[22:23], v[22:23], v[72:73] neg_lo:[0,1] neg_hi:[0,1]
	s_nop 0
	v_xor_b32_e32 v72, 0x80000000, v23
	v_mov_b32_e32 v73, v22
	v_pk_mul_f32 v[72:73], v[50:51], v[72:73] op_sel_hi:[0,1]
	v_pk_fma_f32 v[22:23], v[20:21], v[22:23], v[72:73] op_sel_hi:[0,1,1]
	v_pk_add_f32 v[72:73], v[24:25], v[74:75]
	v_pk_add_f32 v[24:25], v[24:25], v[74:75] neg_lo:[0,1] neg_hi:[0,1]
	s_nop 0
	v_xor_b32_e32 v74, 0x80000000, v25
	v_mov_b32_e32 v75, v24
	v_pk_mul_f32 v[74:75], v[100:101], v[74:75] op_sel_hi:[0,1]
	v_pk_fma_f32 v[24:25], v[98:99], v[24:25], v[74:75] op_sel_hi:[0,1,1]
	v_pk_add_f32 v[74:75], v[28:29], v[76:77]
	v_pk_add_f32 v[28:29], v[28:29], v[76:77] neg_lo:[0,1] neg_hi:[0,1]
	s_nop 0
	v_xor_b32_e32 v76, 0x80000000, v29
	v_mov_b32_e32 v77, v28
	v_pk_mul_f32 v[76:77], v[10:11], v[76:77] op_sel_hi:[0,1]
	v_pk_fma_f32 v[28:29], v[10:11], v[28:29], v[76:77] op_sel_hi:[0,1,1]
	v_pk_add_f32 v[76:77], v[26:27], v[78:79]
	v_pk_add_f32 v[26:27], v[26:27], v[78:79] neg_lo:[0,1] neg_hi:[0,1]
	s_nop 0
	v_xor_b32_e32 v78, 0x80000000, v27
	v_mov_b32_e32 v79, v26
	v_pk_mul_f32 v[78:79], v[98:99], v[78:79] op_sel_hi:[0,1]
	v_pk_fma_f32 v[26:27], v[100:101], v[26:27], v[78:79] op_sel_hi:[0,1,1]
	v_pk_add_f32 v[78:79], v[30:31], v[80:81]
	v_pk_add_f32 v[30:31], v[30:31], v[80:81] neg_lo:[0,1] neg_hi:[0,1]
	s_nop 0
	v_xor_b32_e32 v80, 0x80000000, v31
	v_mov_b32_e32 v81, v30
	v_pk_mul_f32 v[80:81], v[20:21], v[80:81] op_sel_hi:[0,1]
	v_pk_fma_f32 v[30:31], v[50:51], v[30:31], v[80:81] op_sel_hi:[0,1,1]
	v_pk_add_f32 v[80:81], v[32:33], v[82:83]
	v_pk_add_f32 v[32:33], v[32:33], v[82:83] neg_lo:[0,1] neg_hi:[0,1]
	s_nop 0
	v_xor_b32_e32 v82, 0x80000000, v33
	v_mov_b32_e32 v83, v32
	v_pk_mul_f32 v[82:83], v[92:93], v[82:83] op_sel_hi:[0,1]
	v_pk_fma_f32 v[32:33], v[102:103], v[32:33], v[82:83] op_sel_hi:[0,1,1]
	v_pk_add_f32 v[82:83], v[34:35], v[86:87]
	v_pk_add_f32 v[34:35], v[34:35], v[86:87] neg_lo:[0,1] neg_hi:[0,1]
	s_nop 0
	v_xor_b32_e32 v86, 0x80000000, v35
	v_mov_b32_e32 v87, v34
	v_pk_add_f32 v[34:35], v[36:37], v[88:89]
	v_pk_add_f32 v[36:37], v[36:37], v[88:89] neg_lo:[0,1] neg_hi:[0,1]
	s_nop 0
	v_xor_b32_e32 v88, 0x80000000, v37
	v_mov_b32_e32 v89, v36
	v_pk_mul_f32 v[88:89], v[92:93], v[88:89] op_sel_hi:[0,1]
	v_pk_fma_f32 v[36:37], v[102:103], v[36:37], v[88:89] op_sel_hi:[0,1,1] neg_lo:[1,0,0] neg_hi:[1,0,0]
	v_pk_add_f32 v[88:89], v[38:39], v[90:91]
	v_pk_add_f32 v[38:39], v[38:39], v[90:91] neg_lo:[0,1] neg_hi:[0,1]
	s_nop 0
	v_xor_b32_e32 v90, 0x80000000, v39
	v_mov_b32_e32 v91, v38
	v_pk_mul_f32 v[90:91], v[20:21], v[90:91] op_sel_hi:[0,1]
	v_pk_fma_f32 v[38:39], v[50:51], v[38:39], v[90:91] op_sel_hi:[0,1,1] neg_lo:[1,0,0] neg_hi:[1,0,0]
	v_pk_add_f32 v[90:91], v[40:41], v[84:85]
	v_pk_add_f32 v[40:41], v[40:41], v[84:85] neg_lo:[0,1] neg_hi:[0,1]
	s_nop 0
	v_xor_b32_e32 v84, 0x80000000, v41
	v_mov_b32_e32 v85, v40
	v_pk_mul_f32 v[84:85], v[98:99], v[84:85] op_sel_hi:[0,1]
	v_pk_fma_f32 v[40:41], v[100:101], v[40:41], v[84:85] op_sel_hi:[0,1,1] neg_lo:[1,0,0] neg_hi:[1,0,0]
	v_pk_add_f32 v[84:85], v[44:45], v[96:97]
	v_pk_add_f32 v[44:45], v[44:45], v[96:97] neg_lo:[0,1] neg_hi:[0,1]
	s_nop 0
	v_xor_b32_e32 v96, 0x80000000, v45
	v_mov_b32_e32 v97, v44
	v_pk_mul_f32 v[96:97], v[10:11], v[96:97] op_sel_hi:[0,1]
	v_pk_fma_f32 v[44:45], v[10:11], v[44:45], v[96:97] op_sel_hi:[0,1,1] neg_lo:[1,0,0] neg_hi:[1,0,0]
	v_pk_add_f32 v[96:97], v[42:43], v[94:95]
	v_pk_add_f32 v[42:43], v[42:43], v[94:95] neg_lo:[0,1] neg_hi:[0,1]
	s_nop 0
	v_xor_b32_e32 v94, 0x80000000, v43
	v_mov_b32_e32 v95, v42
	v_pk_mul_f32 v[94:95], v[100:101], v[94:95] op_sel_hi:[0,1]
	v_pk_fma_f32 v[42:43], v[98:99], v[42:43], v[94:95] op_sel_hi:[0,1,1] neg_lo:[1,0,0] neg_hi:[1,0,0]
	v_pk_add_f32 v[94:95], v[46:47], v[66:67]
	v_pk_add_f32 v[46:47], v[46:47], v[66:67] neg_lo:[0,1] neg_hi:[0,1]
	s_nop 0
	v_xor_b32_e32 v66, 0x80000000, v47
	v_mov_b32_e32 v67, v46
	v_pk_mul_f32 v[66:67], v[50:51], v[66:67] op_sel_hi:[0,1]
	v_pk_fma_f32 v[46:47], v[20:21], v[46:47], v[66:67] op_sel_hi:[0,1,1] neg_lo:[1,0,0] neg_hi:[1,0,0]
	v_pk_add_f32 v[66:67], v[48:49], v[68:69]
	v_pk_add_f32 v[48:49], v[48:49], v[68:69] neg_lo:[0,1] neg_hi:[0,1]
	s_nop 0
	v_xor_b32_e32 v68, 0x80000000, v49
	v_mov_b32_e32 v69, v48
	v_pk_mul_f32 v[68:69], v[102:103], v[68:69] op_sel_hi:[0,1]
	v_pk_fma_f32 v[48:49], v[92:93], v[48:49], v[68:69] op_sel_hi:[0,1,1] neg_lo:[1,0,0] neg_hi:[1,0,0]
	v_pk_add_f32 v[92:93], v[52:53], v[34:35]
	v_pk_add_f32 v[34:35], v[52:53], v[34:35] neg_lo:[0,1] neg_hi:[0,1]
	v_pk_add_f32 v[68:69], v[104:105], v[82:83]
	v_xor_b32_e32 v52, 0x80000000, v35
	v_mov_b32_e32 v53, v34
	v_pk_mul_f32 v[52:53], v[50:51], v[52:53] op_sel_hi:[0,1]
	v_pk_fma_f32 v[34:35], v[20:21], v[34:35], v[52:53] op_sel_hi:[0,1,1]
	v_pk_add_f32 v[52:53], v[70:71], v[88:89]
	v_pk_add_f32 v[70:71], v[70:71], v[88:89] neg_lo:[0,1] neg_hi:[0,1]
	v_pk_add_f32 v[82:83], v[104:105], v[82:83] neg_lo:[0,1] neg_hi:[0,1]
	v_xor_b32_e32 v88, 0x80000000, v71
	v_mov_b32_e32 v89, v70
	v_pk_mul_f32 v[88:89], v[10:11], v[88:89] op_sel_hi:[0,1]
	v_pk_fma_f32 v[70:71], v[10:11], v[70:71], v[88:89] op_sel_hi:[0,1,1]
	v_pk_add_f32 v[88:89], v[72:73], v[90:91]
	v_pk_add_f32 v[72:73], v[72:73], v[90:91] neg_lo:[0,1] neg_hi:[0,1]
	s_nop 0
	v_xor_b32_e32 v90, 0x80000000, v73
	v_mov_b32_e32 v91, v72
	v_pk_mul_f32 v[90:91], v[20:21], v[90:91] op_sel_hi:[0,1]
	v_pk_fma_f32 v[72:73], v[50:51], v[72:73], v[90:91] op_sel_hi:[0,1,1]
	v_pk_add_f32 v[90:91], v[74:75], v[84:85]
	v_pk_add_f32 v[74:75], v[74:75], v[84:85] neg_lo:[0,1] neg_hi:[0,1]
	s_nop 0
	v_xor_b32_e32 v84, 0x80000000, v75
	v_mov_b32_e32 v85, v74
	v_pk_add_f32 v[74:75], v[76:77], v[96:97]
	v_pk_add_f32 v[76:77], v[76:77], v[96:97] neg_lo:[0,1] neg_hi:[0,1]
	s_nop 0
	v_xor_b32_e32 v96, 0x80000000, v77
	v_mov_b32_e32 v97, v76
	v_pk_mul_f32 v[96:97], v[20:21], v[96:97] op_sel_hi:[0,1]
	v_pk_fma_f32 v[76:77], v[50:51], v[76:77], v[96:97] op_sel_hi:[0,1,1] neg_lo:[1,0,0] neg_hi:[1,0,0]
	v_pk_add_f32 v[96:97], v[78:79], v[94:95]
	v_pk_add_f32 v[78:79], v[78:79], v[94:95] neg_lo:[0,1] neg_hi:[0,1]
	s_nop 0
	v_xor_b32_e32 v94, 0x80000000, v79
	v_mov_b32_e32 v95, v78
	v_pk_mul_f32 v[94:95], v[10:11], v[94:95] op_sel_hi:[0,1]
	v_pk_fma_f32 v[78:79], v[10:11], v[78:79], v[94:95] op_sel_hi:[0,1,1] neg_lo:[1,0,0] neg_hi:[1,0,0]
	v_pk_add_f32 v[94:95], v[80:81], v[66:67]
	v_pk_add_f32 v[66:67], v[80:81], v[66:67] neg_lo:[0,1] neg_hi:[0,1]
	s_nop 0
	v_xor_b32_e32 v80, 0x80000000, v67
	v_mov_b32_e32 v81, v66
	v_pk_mul_f32 v[80:81], v[50:51], v[80:81] op_sel_hi:[0,1]
	v_pk_fma_f32 v[66:67], v[20:21], v[66:67], v[80:81] op_sel_hi:[0,1,1] neg_lo:[1,0,0] neg_hi:[1,0,0]
	v_pk_add_f32 v[80:81], v[68:69], v[90:91]
	v_pk_add_f32 v[68:69], v[68:69], v[90:91] neg_lo:[0,1] neg_hi:[0,1]
	v_pk_add_f32 v[90:91], v[92:93], v[74:75]
	v_pk_add_f32 v[74:75], v[92:93], v[74:75] neg_lo:[0,1] neg_hi:[0,1]
	s_nop 0
	v_xor_b32_e32 v92, 0x80000000, v75
	v_mov_b32_e32 v93, v74
	v_pk_mul_f32 v[92:93], v[10:11], v[92:93] op_sel_hi:[0,1]
	v_pk_fma_f32 v[74:75], v[10:11], v[74:75], v[92:93] op_sel_hi:[0,1,1]
	v_pk_add_f32 v[92:93], v[52:53], v[96:97]
	v_pk_add_f32 v[52:53], v[52:53], v[96:97] neg_lo:[0,1] neg_hi:[0,1]
	s_nop 0
	v_xor_b32_e32 v96, 0x80000000, v53
	v_mov_b32_e32 v97, v52
	v_pk_add_f32 v[52:53], v[88:89], v[94:95]
	v_pk_add_f32 v[88:89], v[88:89], v[94:95] neg_lo:[0,1] neg_hi:[0,1]
	s_nop 0
	v_xor_b32_e32 v94, 0x80000000, v89
	v_mov_b32_e32 v95, v88
	v_pk_mul_f32 v[94:95], v[10:11], v[94:95] op_sel_hi:[0,1]
	v_pk_fma_f32 v[88:89], v[10:11], v[88:89], v[94:95] op_sel_hi:[0,1,1] neg_lo:[1,0,0] neg_hi:[1,0,0]
	v_pk_add_f32 v[94:95], v[80:81], v[92:93]
	v_pk_add_f32 v[80:81], v[80:81], v[92:93] neg_lo:[0,1] neg_hi:[0,1]
	v_pk_add_f32 v[92:93], v[90:91], v[52:53]
	v_pk_add_f32 v[52:53], v[90:91], v[52:53] neg_lo:[0,1] neg_hi:[0,1]
	s_nop 0
	v_xor_b32_e32 v90, 0x80000000, v53
	v_mov_b32_e32 v91, v52
	v_pk_add_f32 v[52:53], v[94:95], v[92:93]
	v_pk_add_f32 v[92:93], v[94:95], v[92:93] neg_lo:[0,1] neg_hi:[0,1]
	v_pk_add_f32 v[94:95], v[80:81], v[90:91]
	v_pk_add_f32 v[80:81], v[80:81], v[90:91] neg_lo:[0,1] neg_hi:[0,1]
	v_pk_add_f32 v[90:91], v[68:69], v[96:97]
	v_pk_add_f32 v[68:69], v[68:69], v[96:97] neg_lo:[0,1] neg_hi:[0,1]
	v_pk_add_f32 v[96:97], v[74:75], v[88:89]
	v_pk_add_f32 v[74:75], v[74:75], v[88:89] neg_lo:[0,1] neg_hi:[0,1]
	s_nop 0
	v_xor_b32_e32 v88, 0x80000000, v75
	v_mov_b32_e32 v89, v74
	v_pk_add_f32 v[74:75], v[90:91], v[96:97]
	v_pk_add_f32 v[90:91], v[90:91], v[96:97] neg_lo:[0,1] neg_hi:[0,1]
	v_pk_add_f32 v[96:97], v[68:69], v[88:89]
	v_pk_add_f32 v[68:69], v[68:69], v[88:89] neg_lo:[0,1] neg_hi:[0,1]
	v_pk_add_f32 v[88:89], v[82:83], v[84:85]
	v_pk_add_f32 v[82:83], v[82:83], v[84:85] neg_lo:[0,1] neg_hi:[0,1]
	v_pk_add_f32 v[84:85], v[34:35], v[76:77]
	v_pk_add_f32 v[34:35], v[34:35], v[76:77] neg_lo:[0,1] neg_hi:[0,1]
	s_nop 0
	v_xor_b32_e32 v76, 0x80000000, v35
	v_mov_b32_e32 v77, v34
	v_pk_mul_f32 v[76:77], v[10:11], v[76:77] op_sel_hi:[0,1]
	v_pk_fma_f32 v[34:35], v[10:11], v[34:35], v[76:77] op_sel_hi:[0,1,1]
	v_pk_add_f32 v[76:77], v[70:71], v[78:79]
	v_pk_add_f32 v[70:71], v[70:71], v[78:79] neg_lo:[0,1] neg_hi:[0,1]
	s_nop 0
	v_xor_b32_e32 v78, 0x80000000, v71
	v_mov_b32_e32 v79, v70
	v_pk_add_f32 v[70:71], v[72:73], v[66:67]
	v_pk_add_f32 v[66:67], v[72:73], v[66:67] neg_lo:[0,1] neg_hi:[0,1]
	s_nop 0
	v_xor_b32_e32 v72, 0x80000000, v67
	v_mov_b32_e32 v73, v66
	v_pk_mul_f32 v[72:73], v[10:11], v[72:73] op_sel_hi:[0,1]
	v_pk_fma_f32 v[66:67], v[10:11], v[66:67], v[72:73] op_sel_hi:[0,1,1] neg_lo:[1,0,0] neg_hi:[1,0,0]
	v_pk_add_f32 v[72:73], v[88:89], v[76:77]
	v_pk_add_f32 v[76:77], v[88:89], v[76:77] neg_lo:[0,1] neg_hi:[0,1]
	v_pk_add_f32 v[88:89], v[84:85], v[70:71]
	v_pk_add_f32 v[70:71], v[84:85], v[70:71] neg_lo:[0,1] neg_hi:[0,1]
	s_nop 0
	v_xor_b32_e32 v84, 0x80000000, v71
	v_mov_b32_e32 v85, v70
	v_pk_add_f32 v[70:71], v[72:73], v[88:89]
	v_pk_add_f32 v[72:73], v[72:73], v[88:89] neg_lo:[0,1] neg_hi:[0,1]
	v_pk_add_f32 v[88:89], v[76:77], v[84:85]
	v_pk_add_f32 v[76:77], v[76:77], v[84:85] neg_lo:[0,1] neg_hi:[0,1]
	v_pk_add_f32 v[84:85], v[82:83], v[78:79]
	v_pk_add_f32 v[78:79], v[82:83], v[78:79] neg_lo:[0,1] neg_hi:[0,1]
	v_pk_add_f32 v[82:83], v[34:35], v[66:67]
	v_pk_add_f32 v[34:35], v[34:35], v[66:67] neg_lo:[0,1] neg_hi:[0,1]
	s_nop 0
	v_xor_b32_e32 v66, 0x80000000, v35
	v_mov_b32_e32 v67, v34
	v_pk_add_f32 v[34:35], v[84:85], v[82:83]
	v_pk_add_f32 v[82:83], v[84:85], v[82:83] neg_lo:[0,1] neg_hi:[0,1]
	v_pk_add_f32 v[84:85], v[78:79], v[66:67]
	v_pk_add_f32 v[66:67], v[78:79], v[66:67] neg_lo:[0,1] neg_hi:[0,1]
	v_pk_add_f32 v[78:79], v[16:17], v[86:87]
	v_pk_add_f32 v[16:17], v[16:17], v[86:87] neg_lo:[0,1] neg_hi:[0,1]
	v_pk_add_f32 v[86:87], v[18:19], v[36:37]
	v_pk_add_f32 v[18:19], v[18:19], v[36:37] neg_lo:[0,1] neg_hi:[0,1]
	s_nop 0
	v_xor_b32_e32 v36, 0x80000000, v19
	v_mov_b32_e32 v37, v18
	v_pk_mul_f32 v[36:37], v[50:51], v[36:37] op_sel_hi:[0,1]
	v_pk_fma_f32 v[18:19], v[20:21], v[18:19], v[36:37] op_sel_hi:[0,1,1]
	v_pk_add_f32 v[36:37], v[22:23], v[38:39]
	v_pk_add_f32 v[22:23], v[22:23], v[38:39] neg_lo:[0,1] neg_hi:[0,1]
	s_nop 0
	v_xor_b32_e32 v38, 0x80000000, v23
	v_mov_b32_e32 v39, v22
	v_pk_mul_f32 v[38:39], v[10:11], v[38:39] op_sel_hi:[0,1]
	v_pk_fma_f32 v[22:23], v[10:11], v[22:23], v[38:39] op_sel_hi:[0,1,1]
	v_pk_add_f32 v[38:39], v[24:25], v[40:41]
	v_pk_add_f32 v[24:25], v[24:25], v[40:41] neg_lo:[0,1] neg_hi:[0,1]
	s_nop 0
	v_xor_b32_e32 v40, 0x80000000, v25
	v_mov_b32_e32 v41, v24
	v_pk_mul_f32 v[40:41], v[20:21], v[40:41] op_sel_hi:[0,1]
	v_pk_fma_f32 v[24:25], v[50:51], v[24:25], v[40:41] op_sel_hi:[0,1,1]
	v_pk_add_f32 v[40:41], v[28:29], v[44:45]
	v_pk_add_f32 v[28:29], v[28:29], v[44:45] neg_lo:[0,1] neg_hi:[0,1]
	s_nop 0
	v_xor_b32_e32 v44, 0x80000000, v29
	v_mov_b32_e32 v45, v28
	v_pk_add_f32 v[28:29], v[26:27], v[42:43]
	v_pk_add_f32 v[26:27], v[26:27], v[42:43] neg_lo:[0,1] neg_hi:[0,1]
	s_nop 0
	v_xor_b32_e32 v42, 0x80000000, v27
	v_mov_b32_e32 v43, v26
	v_pk_mul_f32 v[42:43], v[20:21], v[42:43] op_sel_hi:[0,1]
	v_pk_fma_f32 v[26:27], v[50:51], v[26:27], v[42:43] op_sel_hi:[0,1,1] neg_lo:[1,0,0] neg_hi:[1,0,0]
	v_pk_add_f32 v[42:43], v[30:31], v[46:47]
	v_pk_add_f32 v[30:31], v[30:31], v[46:47] neg_lo:[0,1] neg_hi:[0,1]
	s_nop 0
	v_xor_b32_e32 v46, 0x80000000, v31
	v_mov_b32_e32 v47, v30
	v_pk_mul_f32 v[46:47], v[10:11], v[46:47] op_sel_hi:[0,1]
	v_pk_fma_f32 v[30:31], v[10:11], v[30:31], v[46:47] op_sel_hi:[0,1,1] neg_lo:[1,0,0] neg_hi:[1,0,0]
	v_pk_add_f32 v[46:47], v[32:33], v[48:49]
	v_pk_add_f32 v[32:33], v[32:33], v[48:49] neg_lo:[0,1] neg_hi:[0,1]
	s_nop 0
	v_xor_b32_e32 v48, 0x80000000, v33
	v_mov_b32_e32 v49, v32
	v_pk_mul_f32 v[48:49], v[50:51], v[48:49] op_sel_hi:[0,1]
	v_pk_fma_f32 v[20:21], v[20:21], v[32:33], v[48:49] op_sel_hi:[0,1,1] neg_lo:[1,0,0] neg_hi:[1,0,0]
	v_pk_add_f32 v[48:49], v[86:87], v[28:29]
	v_pk_add_f32 v[28:29], v[86:87], v[28:29] neg_lo:[0,1] neg_hi:[0,1]
	v_pk_add_f32 v[32:33], v[78:79], v[40:41]
	v_pk_add_f32 v[40:41], v[78:79], v[40:41] neg_lo:[0,1] neg_hi:[0,1]
	v_xor_b32_e32 v78, 0x80000000, v29
	v_mov_b32_e32 v79, v28
	v_pk_mul_f32 v[78:79], v[10:11], v[78:79] op_sel_hi:[0,1]
	v_pk_fma_f32 v[28:29], v[10:11], v[28:29], v[78:79] op_sel_hi:[0,1,1]
	v_pk_add_f32 v[78:79], v[36:37], v[42:43]
	v_pk_add_f32 v[36:37], v[36:37], v[42:43] neg_lo:[0,1] neg_hi:[0,1]
	s_nop 0
	v_xor_b32_e32 v42, 0x80000000, v37
	v_mov_b32_e32 v43, v36
	v_pk_add_f32 v[36:37], v[38:39], v[46:47]
	v_pk_add_f32 v[38:39], v[38:39], v[46:47] neg_lo:[0,1] neg_hi:[0,1]
	s_nop 0
	v_xor_b32_e32 v46, 0x80000000, v39
	v_mov_b32_e32 v47, v38
	v_pk_mul_f32 v[46:47], v[10:11], v[46:47] op_sel_hi:[0,1]
	v_pk_fma_f32 v[38:39], v[10:11], v[38:39], v[46:47] op_sel_hi:[0,1,1] neg_lo:[1,0,0] neg_hi:[1,0,0]
	v_pk_add_f32 v[46:47], v[32:33], v[78:79]
	v_pk_add_f32 v[32:33], v[32:33], v[78:79] neg_lo:[0,1] neg_hi:[0,1]
	v_pk_add_f32 v[78:79], v[48:49], v[36:37]
	v_pk_add_f32 v[36:37], v[48:49], v[36:37] neg_lo:[0,1] neg_hi:[0,1]
	s_nop 0
	v_xor_b32_e32 v48, 0x80000000, v37
	v_mov_b32_e32 v49, v36
	v_pk_add_f32 v[86:87], v[32:33], v[48:49]
	v_pk_add_f32 v[32:33], v[32:33], v[48:49] neg_lo:[0,1] neg_hi:[0,1]
	v_pk_add_f32 v[48:49], v[40:41], v[42:43]
	v_pk_add_f32 v[40:41], v[40:41], v[42:43] neg_lo:[0,1] neg_hi:[0,1]
	v_pk_add_f32 v[42:43], v[28:29], v[38:39]
	v_pk_add_f32 v[28:29], v[28:29], v[38:39] neg_lo:[0,1] neg_hi:[0,1]
	v_pk_add_f32 v[36:37], v[46:47], v[78:79] neg_lo:[0,1] neg_hi:[0,1]
	v_xor_b32_e32 v38, 0x80000000, v29
	v_mov_b32_e32 v39, v28
	v_pk_add_f32 v[28:29], v[48:49], v[42:43]
	v_pk_add_f32 v[42:43], v[48:49], v[42:43] neg_lo:[0,1] neg_hi:[0,1]
	v_pk_add_f32 v[48:49], v[40:41], v[38:39]
	v_pk_add_f32 v[38:39], v[40:41], v[38:39] neg_lo:[0,1] neg_hi:[0,1]
	v_pk_add_f32 v[40:41], v[16:17], v[44:45]
	v_pk_add_f32 v[16:17], v[16:17], v[44:45] neg_lo:[0,1] neg_hi:[0,1]
	v_pk_add_f32 v[44:45], v[18:19], v[26:27]
	v_pk_add_f32 v[18:19], v[18:19], v[26:27] neg_lo:[0,1] neg_hi:[0,1]
	s_nop 0
	v_xor_b32_e32 v26, 0x80000000, v19
	v_mov_b32_e32 v27, v18
	v_pk_mul_f32 v[26:27], v[10:11], v[26:27] op_sel_hi:[0,1]
	v_pk_fma_f32 v[18:19], v[10:11], v[18:19], v[26:27] op_sel_hi:[0,1,1]
	v_pk_add_f32 v[26:27], v[22:23], v[30:31]
	v_pk_add_f32 v[22:23], v[22:23], v[30:31] neg_lo:[0,1] neg_hi:[0,1]
	s_nop 0
	v_xor_b32_e32 v30, 0x80000000, v23
	v_mov_b32_e32 v31, v22
	v_pk_add_f32 v[22:23], v[24:25], v[20:21]
	v_pk_add_f32 v[20:21], v[24:25], v[20:21] neg_lo:[0,1] neg_hi:[0,1]
	s_nop 0
	v_xor_b32_e32 v24, 0x80000000, v21
	v_mov_b32_e32 v25, v20
	v_pk_mul_f32 v[24:25], v[10:11], v[24:25] op_sel_hi:[0,1]
	v_pk_fma_f32 v[20:21], v[10:11], v[20:21], v[24:25] op_sel_hi:[0,1,1] neg_lo:[1,0,0] neg_hi:[1,0,0]
	v_pk_add_f32 v[24:25], v[40:41], v[26:27]
	v_pk_add_f32 v[26:27], v[40:41], v[26:27] neg_lo:[0,1] neg_hi:[0,1]
	v_pk_add_f32 v[40:41], v[44:45], v[22:23]
	v_pk_add_f32 v[22:23], v[44:45], v[22:23] neg_lo:[0,1] neg_hi:[0,1]
	s_nop 0
	v_xor_b32_e32 v44, 0x80000000, v23
	v_mov_b32_e32 v45, v22
	v_pk_add_f32 v[22:23], v[24:25], v[40:41]
	v_pk_add_f32 v[24:25], v[24:25], v[40:41] neg_lo:[0,1] neg_hi:[0,1]
	v_pk_add_f32 v[40:41], v[26:27], v[44:45]
	v_pk_add_f32 v[26:27], v[26:27], v[44:45] neg_lo:[0,1] neg_hi:[0,1]
	v_pk_add_f32 v[44:45], v[16:17], v[30:31]
	v_pk_add_f32 v[16:17], v[16:17], v[30:31] neg_lo:[0,1] neg_hi:[0,1]
	v_pk_add_f32 v[30:31], v[18:19], v[20:21]
	v_pk_add_f32 v[18:19], v[18:19], v[20:21] neg_lo:[0,1] neg_hi:[0,1]
	s_nop 0
	v_xor_b32_e32 v20, 0x80000000, v19
	v_mov_b32_e32 v21, v18
	v_pk_add_f32 v[18:19], v[44:45], v[30:31]
	v_pk_add_f32 v[30:31], v[44:45], v[30:31] neg_lo:[0,1] neg_hi:[0,1]
	v_pk_add_f32 v[44:45], v[16:17], v[20:21]
	v_pk_add_f32 v[16:17], v[16:17], v[20:21] neg_lo:[0,1] neg_hi:[0,1]
	v_pk_add_f32 v[20:21], v[46:47], v[78:79]
	ds_write2_b64 v13, v[52:53], v[20:21] offset1:16
	ds_write2_b64 v15, v[70:71], v[22:23] offset0:32 offset1:48
	ds_write2_b64 v51, v[74:75], v[28:29] offset0:64 offset1:80
	ds_write2_b64 v54, v[34:35], v[18:19] offset0:96 offset1:112
	ds_write2_b64 v55, v[94:95], v[86:87] offset0:128 offset1:144
	ds_write2_b64 v56, v[88:89], v[40:41] offset0:160 offset1:176
	ds_write2_b64 v57, v[96:97], v[48:49] offset0:192 offset1:208
	ds_write2_b64 v58, v[84:85], v[44:45] offset0:224 offset1:240
	ds_write2_b64 v59, v[92:93], v[36:37] offset1:16
	ds_write2_b64 v60, v[72:73], v[24:25] offset0:32 offset1:48
	ds_write2_b64 v61, v[90:91], v[42:43] offset0:64 offset1:80
	ds_write2_b64 v62, v[82:83], v[30:31] offset0:96 offset1:112
	ds_write2_b64 v63, v[80:81], v[32:33] offset0:128 offset1:144
	ds_write2_b64 v64, v[76:77], v[26:27] offset0:160 offset1:176
	ds_write2_b64 v65, v[68:69], v[38:39] offset0:192 offset1:208
	ds_write2_b64 v101, v[66:67], v[16:17] offset0:224 offset1:240
	v_mov_b32_e32 v10, v173
	s_waitcnt lgkmcnt(0)
	s_barrier
	v_mov_b32_e32 v22, v178
	v_mov_b32_e32 v23, v179
	v_lshl_add_u32 v10, v10, 3, 0
	ds_read_b64 v[16:17], v10
	ds_read_b64 v[80:81], v10 offset:4224
	ds_read_b64 v[78:79], v10 offset:8448
	ds_read_b64 v[76:77], v10 offset:12672
	ds_read_b64 v[74:75], v10 offset:16896
	ds_read_b64 v[72:73], v10 offset:21120
	ds_read_b64 v[70:71], v10 offset:25344
	ds_read_b64 v[68:69], v10 offset:29568
	ds_read_b64 v[24:25], v10 offset:33792
	ds_read_b64 v[62:63], v10 offset:38016
	ds_read_b64 v[60:61], v10 offset:42240
	ds_read_b64 v[58:59], v10 offset:46464
	ds_read_b64 v[54:55], v10 offset:50688
	ds_read_b64 v[50:51], v10 offset:54912
	ds_read_b64 v[46:47], v10 offset:59136
	ds_read_b64 v[44:45], v10 offset:63360
	v_add_u32_e32 v13, 0x10800, v10
	v_add_u32_e32 v15, 0x11880, v10
	v_add_u32_e32 v20, 0x12900, v10
	v_add_u32_e32 v21, 0x13980, v10
	ds_read_b64 v[18:19], v13
	ds_read_b64 v[66:67], v15
	ds_read_b64 v[64:65], v20
	ds_read_b64 v[38:39], v21
	v_add_u32_e32 v13, 0x14a00, v10
	v_add_u32_e32 v15, 0x15a80, v10
	v_add_u32_e32 v20, 0x16b00, v10
	v_add_u32_e32 v21, 0x17b80, v10
	ds_read_b64 v[30:31], v13
	ds_read_b64 v[56:57], v15
	ds_read_b64 v[52:53], v20
	ds_read_b64 v[48:49], v21
	v_add_u32_e32 v13, 0x18c00, v10
	v_add_u32_e32 v15, 0x19c80, v10
	v_add_u32_e32 v20, 0x1ad00, v10
	v_add_u32_e32 v21, 0x1bd80, v10
	ds_read_b64 v[82:83], v13
	ds_read_b64 v[42:43], v15
	ds_read_b64 v[40:41], v20
	ds_read_b64 v[36:37], v21
	v_add_u32_e32 v13, 0x1ce00, v10
	v_add_u32_e32 v15, 0x1de80, v10
	v_add_u32_e32 v20, 0x1ef00, v10
	v_add_u32_e32 v10, 0x1ff80, v10
	ds_read_b64 v[34:35], v13
	ds_read_b64 v[32:33], v15
	ds_read_b64 v[28:29], v20
	ds_read_b64 v[26:27], v10
	v_pk_fma_f32 v[84:85], v[22:23], s[90:91], v[22:23] op_sel:[1,0,0] op_sel_hi:[0,1,1]
	v_xor_b32_e32 v20, 0x80000000, v85
	v_mov_b32_e32 v21, v85
	v_pk_mul_f32 v[20:21], v[22:23], v[20:21] op_sel:[1,0] op_sel_hi:[0,1]
	v_pk_fma_f32 v[86:87], v[22:23], v[84:85], v[20:21] op_sel_hi:[1,0,1]
	v_mov_b32_e32 v10, v1
	v_xor_b32_e32 v20, 0x80000000, v87
	v_mov_b32_e32 v21, v87
	v_pk_mul_f32 v[20:21], v[22:23], v[20:21] op_sel:[1,0] op_sel_hi:[0,1]
	v_pk_fma_f32 v[88:89], v[22:23], v[86:87], v[20:21] op_sel_hi:[1,0,1]
	v_mov_b32_e32 v13, v171
	v_xor_b32_e32 v20, 0x80000000, v89
	v_mov_b32_e32 v21, v89
	v_pk_mul_f32 v[20:21], v[22:23], v[20:21] op_sel:[1,0] op_sel_hi:[0,1]
	v_pk_fma_f32 v[90:91], v[22:23], v[88:89], v[20:21] op_sel_hi:[1,0,1]
	v_mov_b32_e32 v10, v164
	v_xor_b32_e32 v20, 0x80000000, v91
	v_mov_b32_e32 v21, v91
	v_pk_mul_f32 v[20:21], v[22:23], v[20:21] op_sel:[1,0] op_sel_hi:[0,1]
	v_pk_fma_f32 v[92:93], v[22:23], v[90:91], v[20:21] op_sel_hi:[1,0,1]
	s_waitcnt lgkmcnt(14)
	v_fmac_f32_e32 v16, 0, v17
	v_xor_b32_e32 v20, 0x80000000, v93
	v_mov_b32_e32 v21, v93
	v_pk_mul_f32 v[20:21], v[22:23], v[20:21] op_sel:[1,0] op_sel_hi:[0,1]
	v_pk_fma_f32 v[94:95], v[22:23], v[92:93], v[20:21] op_sel_hi:[1,0,1]
	v_readlane_b32 s70, v251, 22
	v_xor_b32_e32 v20, 0x80000000, v95
	v_mov_b32_e32 v21, v95
	v_pk_mul_f32 v[20:21], v[22:23], v[20:21] op_sel:[1,0] op_sel_hi:[0,1]
	v_pk_fma_f32 v[96:97], v[22:23], v[94:95], v[20:21] op_sel_hi:[1,0,1]
	v_readlane_b32 s71, v251, 23
	v_xor_b32_e32 v20, 0x80000000, v97
	v_mov_b32_e32 v21, v97
	v_pk_mul_f32 v[20:21], v[22:23], v[20:21] op_sel:[1,0] op_sel_hi:[0,1]
	v_pk_fma_f32 v[98:99], v[22:23], v[96:97], v[20:21] op_sel_hi:[1,0,1]
	s_movk_i32 s10, 0x1000
	v_xor_b32_e32 v20, 0x80000000, v99
	v_mov_b32_e32 v21, v99
	v_pk_mul_f32 v[20:21], v[22:23], v[20:21] op_sel:[1,0] op_sel_hi:[0,1]
	v_pk_fma_f32 v[100:101], v[22:23], v[98:99], v[20:21] op_sel_hi:[1,0,1]
	s_movk_i32 s11, 0x2000
	v_xor_b32_e32 v20, 0x80000000, v101
	v_mov_b32_e32 v21, v101
	v_pk_mul_f32 v[20:21], v[22:23], v[20:21] op_sel:[1,0] op_sel_hi:[0,1]
	v_pk_fma_f32 v[102:103], v[22:23], v[100:101], v[20:21] op_sel_hi:[1,0,1]
	s_movk_i32 s13, 0x5000
	v_xor_b32_e32 v20, 0x80000000, v103
	v_mov_b32_e32 v21, v103
	v_pk_mul_f32 v[20:21], v[22:23], v[20:21] op_sel:[1,0] op_sel_hi:[0,1]
	v_pk_fma_f32 v[104:105], v[22:23], v[102:103], v[20:21] op_sel_hi:[1,0,1]
	s_movk_i32 s12, 0x6000
	v_xor_b32_e32 v20, 0x80000000, v105
	v_mov_b32_e32 v21, v105
	v_pk_mul_f32 v[20:21], v[22:23], v[20:21] op_sel:[1,0] op_sel_hi:[0,1]
	v_pk_fma_f32 v[106:107], v[22:23], v[104:105], v[20:21] op_sel_hi:[1,0,1]
	s_movk_i32 s16, 0x7000
	v_xor_b32_e32 v20, 0x80000000, v107
	v_mov_b32_e32 v21, v107
	v_pk_mul_f32 v[20:21], v[22:23], v[20:21] op_sel:[1,0] op_sel_hi:[0,1]
	v_pk_fma_f32 v[108:109], v[22:23], v[106:107], v[20:21] op_sel_hi:[1,0,1]
	s_mov_b32 s80, 0x3f74fa0b
	v_xor_b32_e32 v20, 0x80000000, v109
	v_mov_b32_e32 v21, v109
	v_pk_mul_f32 v[20:21], v[22:23], v[20:21] op_sel:[1,0] op_sel_hi:[0,1]
	v_pk_fma_f32 v[110:111], v[22:23], v[108:109], v[20:21] op_sel_hi:[1,0,1]
	s_mov_b32 s81, 0xbe94a031
	v_xor_b32_e32 v20, 0x80000000, v111
	v_mov_b32_e32 v21, v111
	v_pk_mul_f32 v[20:21], v[22:23], v[20:21] op_sel:[1,0] op_sel_hi:[0,1]
	v_pk_fma_f32 v[112:113], v[22:23], v[110:111], v[20:21] op_sel_hi:[1,0,1]
	s_mov_b32 s20, 0x3f61c598
	v_xor_b32_e32 v20, 0x80000000, v113
	v_mov_b32_e32 v21, v113
	v_pk_mul_f32 v[20:21], v[22:23], v[20:21] op_sel:[1,0] op_sel_hi:[0,1]
	v_pk_fma_f32 v[20:21], v[22:23], v[112:113], v[20:21] op_sel_hi:[1,0,1]
	s_mov_b32 s21, 0xbef15aea
	v_xor_b32_e32 v114, 0x80000000, v21
	v_mov_b32_e32 v115, v21
	v_pk_mul_f32 v[114:115], v[22:23], v[114:115] op_sel:[1,0] op_sel_hi:[0,1]
	v_pk_fma_f32 v[114:115], v[22:23], v[20:21], v[114:115] op_sel_hi:[1,0,1]
	v_mul_f32_e32 v18, v18, v20
	v_xor_b32_e32 v116, 0x80000000, v115
	v_mov_b32_e32 v117, v115
	v_pk_mul_f32 v[116:117], v[22:23], v[116:117] op_sel:[1,0] op_sel_hi:[0,1]
	v_pk_fma_f32 v[116:117], v[22:23], v[114:115], v[116:117] op_sel_hi:[1,0,1]
	v_fmac_f32_e32 v18, v19, v21
	v_xor_b32_e32 v118, 0x80000000, v117
	v_mov_b32_e32 v119, v117
	v_pk_mul_f32 v[118:119], v[22:23], v[118:119] op_sel:[1,0] op_sel_hi:[0,1]
	v_pk_fma_f32 v[118:119], v[22:23], v[116:117], v[118:119] op_sel_hi:[1,0,1]
	v_add_f32_e32 v17, v16, v18
	v_xor_b32_e32 v120, 0x80000000, v119
	v_mov_b32_e32 v121, v119
	v_pk_mul_f32 v[120:121], v[22:23], v[120:121] op_sel:[1,0] op_sel_hi:[0,1]
	v_pk_fma_f32 v[120:121], v[22:23], v[118:119], v[120:121] op_sel_hi:[1,0,1]
	s_mov_b32 s40, s45
	v_xor_b32_e32 v122, 0x80000000, v121
	v_mov_b32_e32 v123, v121
	v_pk_mul_f32 v[122:123], v[22:23], v[122:123] op_sel:[1,0] op_sel_hi:[0,1]
	v_pk_fma_f32 v[122:123], v[22:23], v[120:121], v[122:123] op_sel_hi:[1,0,1]
	s_mov_b32 s41, s94
	v_xor_b32_e32 v124, 0x80000000, v123
	v_mov_b32_e32 v125, v123
	v_pk_mul_f32 v[124:125], v[22:23], v[124:125] op_sel:[1,0] op_sel_hi:[0,1]
	v_pk_fma_f32 v[124:125], v[22:23], v[122:123], v[124:125] op_sel_hi:[1,0,1]
	s_mov_b32 s86, 0x3f226799
	v_xor_b32_e32 v126, 0x80000000, v125
	v_mov_b32_e32 v127, v125
	v_pk_mul_f32 v[126:127], v[22:23], v[126:127] op_sel:[1,0] op_sel_hi:[0,1]
	v_pk_fma_f32 v[126:127], v[22:23], v[124:125], v[126:127] op_sel_hi:[1,0,1]
	s_mov_b32 s87, 0xbf45e403
	v_xor_b32_e32 v128, 0x80000000, v127
	v_mov_b32_e32 v129, v127
	v_pk_mul_f32 v[128:129], v[22:23], v[128:129] op_sel:[1,0] op_sel_hi:[0,1]
	v_pk_fma_f32 v[128:129], v[22:23], v[126:127], v[128:129] op_sel_hi:[1,0,1]
	s_mov_b32 s24, 0x3f0e39da
	v_xor_b32_e32 v130, 0x80000000, v129
	v_mov_b32_e32 v131, v129
	v_pk_mul_f32 v[130:131], v[22:23], v[130:131] op_sel:[1,0] op_sel_hi:[0,1]
	v_pk_fma_f32 v[130:131], v[22:23], v[128:129], v[130:131] op_sel_hi:[1,0,1]
	s_mov_b32 s25, 0xbf54db31
	v_xor_b32_e32 v132, 0x80000000, v131
	v_mov_b32_e32 v133, v131
	v_pk_mul_f32 v[132:133], v[22:23], v[132:133] op_sel:[1,0] op_sel_hi:[0,1]
	v_pk_fma_f32 v[132:133], v[22:23], v[130:131], v[132:133] op_sel_hi:[1,0,1]
	s_mov_b32 s88, 0x3ef15aea
	v_xor_b32_e32 v134, 0x80000000, v133
	v_mov_b32_e32 v135, v133
	v_pk_mul_f32 v[134:135], v[22:23], v[134:135] op_sel:[1,0] op_sel_hi:[0,1]
	v_pk_fma_f32 v[134:135], v[22:23], v[132:133], v[134:135] op_sel_hi:[1,0,1]
	s_mov_b32 s89, 0xbf61c598
	v_xor_b32_e32 v136, 0x80000000, v135
	v_mov_b32_e32 v137, v135
	v_pk_mul_f32 v[136:137], v[22:23], v[136:137] op_sel:[1,0] op_sel_hi:[0,1]
	v_pk_fma_f32 v[136:137], v[22:23], v[134:135], v[136:137] op_sel_hi:[1,0,1]
	s_mov_b32 s18, 0x3ec3ef15
	v_xor_b32_e32 v138, 0x80000000, v137
	v_mov_b32_e32 v139, v137
	v_pk_mul_f32 v[138:139], v[22:23], v[138:139] op_sel:[1,0] op_sel_hi:[0,1]
	v_pk_fma_f32 v[138:139], v[22:23], v[136:137], v[138:139] op_sel_hi:[1,0,1]
	s_mov_b32 s19, 0xbf6c835e
	v_xor_b32_e32 v140, 0x80000000, v139
	v_mov_b32_e32 v141, v139
	v_pk_mul_f32 v[140:141], v[22:23], v[140:141] op_sel:[1,0] op_sel_hi:[0,1]
	v_pk_fma_f32 v[140:141], v[22:23], v[138:139], v[140:141] op_sel_hi:[1,0,1]
	s_mov_b32 s92, 0x3e94a031
	v_xor_b32_e32 v142, 0x80000000, v141
	v_mov_b32_e32 v143, v141
	v_pk_mul_f32 v[142:143], v[22:23], v[142:143] op_sel:[1,0] op_sel_hi:[0,1]
	v_pk_fma_f32 v[22:23], v[22:23], v[140:141], v[142:143] op_sel_hi:[1,0,1]
	s_waitcnt lgkmcnt(0)
	v_xor_b32_e32 v143, 0x80000000, v26
	v_mov_b32_e32 v142, v27
	v_pk_mul_f32 v[142:143], v[142:143], v[22:23] op_sel:[0,1]
	s_mov_b32 s93, 0xbf74fa0b
	v_pk_fma_f32 v[26:27], v[26:27], v[22:23], v[142:143] op_sel_hi:[1,0,1]
	v_xor_b32_e32 v23, 0x80000000, v28
	v_mov_b32_e32 v22, v29
	v_pk_mul_f32 v[22:23], v[22:23], v[140:141] op_sel:[0,1]
	s_mov_b32 s82, 0x3f54db31
	v_pk_fma_f32 v[28:29], v[28:29], v[140:141], v[22:23] op_sel_hi:[1,0,1]
	v_xor_b32_e32 v23, 0x80000000, v32
	v_mov_b32_e32 v22, v33
	v_pk_mul_f32 v[22:23], v[22:23], v[138:139] op_sel:[0,1]
	s_mov_b32 s83, 0xbf0e39da
	v_pk_fma_f32 v[32:33], v[32:33], v[138:139], v[22:23] op_sel_hi:[1,0,1]
	v_xor_b32_e32 v23, 0x80000000, v34
	v_mov_b32_e32 v22, v35
	v_pk_mul_f32 v[22:23], v[22:23], v[136:137] op_sel:[0,1]
	s_mov_b32 s28, 0x3f45e403
	v_pk_fma_f32 v[34:35], v[34:35], v[136:137], v[22:23] op_sel_hi:[1,0,1]
	v_xor_b32_e32 v23, 0x80000000, v36
	v_mov_b32_e32 v22, v37
	v_pk_mul_f32 v[22:23], v[22:23], v[134:135] op_sel:[0,1]
	s_mov_b32 s29, 0xbf226799
	v_pk_fma_f32 v[36:37], v[36:37], v[134:135], v[22:23] op_sel_hi:[1,0,1]
	v_xor_b32_e32 v23, 0x80000000, v40
	v_mov_b32_e32 v22, v41
	v_pk_mul_f32 v[22:23], v[22:23], v[132:133] op_sel:[0,1]
	s_mov_b32 s36, s97
	v_pk_fma_f32 v[40:41], v[40:41], v[132:133], v[22:23] op_sel_hi:[1,0,1]
	v_xor_b32_e32 v23, 0x80000000, v42
	v_mov_b32_e32 v22, v43
	v_pk_mul_f32 v[22:23], v[22:23], v[130:131] op_sel:[0,1]
	s_mov_b32 s37, s95
	v_pk_fma_f32 v[42:43], v[42:43], v[130:131], v[22:23] op_sel_hi:[1,0,1]
	v_xor_b32_e32 v23, 0x80000000, v82
	v_mov_b32_e32 v22, v83
	v_pk_mul_f32 v[22:23], v[22:23], v[128:129] op_sel:[0,1]
	s_mov_b32 s96, s95
	v_pk_fma_f32 v[22:23], v[82:83], v[128:129], v[22:23] op_sel_hi:[1,0,1]
	v_xor_b32_e32 v83, 0x80000000, v48
	v_mov_b32_e32 v82, v49
	v_pk_mul_f32 v[82:83], v[82:83], v[126:127] op_sel:[0,1]
	s_mov_b32 s23, s25
	v_pk_fma_f32 v[48:49], v[48:49], v[126:127], v[82:83] op_sel_hi:[1,0,1]
	v_xor_b32_e32 v83, 0x80000000, v52
	v_mov_b32_e32 v82, v53
	v_pk_mul_f32 v[82:83], v[82:83], v[124:125] op_sel:[0,1]
	s_mov_b32 s22, s83
	v_pk_fma_f32 v[52:53], v[52:53], v[124:125], v[82:83] op_sel_hi:[1,0,1]
	v_xor_b32_e32 v83, 0x80000000, v56
	v_mov_b32_e32 v82, v57
	v_pk_mul_f32 v[82:83], v[82:83], v[122:123] op_sel:[0,1]
	s_mov_b32 s26, s29
	v_pk_fma_f32 v[56:57], v[56:57], v[122:123], v[82:83] op_sel_hi:[1,0,1]
	v_xor_b32_e32 v83, 0x80000000, v30
	v_mov_b32_e32 v82, v31
	v_pk_mul_f32 v[82:83], v[82:83], v[120:121] op_sel:[0,1]
	s_mov_b32 s27, s87
	v_pk_fma_f32 v[30:31], v[30:31], v[120:121], v[82:83] op_sel_hi:[1,0,1]
	v_xor_b32_e32 v83, 0x80000000, v38
	v_mov_b32_e32 v82, v39
	v_pk_mul_f32 v[82:83], v[82:83], v[118:119] op_sel:[0,1]
	s_movk_i32 s39, 0x2000
	v_pk_fma_f32 v[38:39], v[38:39], v[118:119], v[82:83] op_sel_hi:[1,0,1]
	v_xor_b32_e32 v83, 0x80000000, v64
	v_mov_b32_e32 v82, v65
	v_pk_mul_f32 v[82:83], v[82:83], v[116:117] op_sel:[0,1]
	s_mov_b32 s44, s94
	v_pk_fma_f32 v[64:65], v[64:65], v[116:117], v[82:83] op_sel_hi:[1,0,1]
	v_xor_b32_e32 v83, 0x80000000, v66
	v_mov_b32_e32 v82, v67
	v_pk_mul_f32 v[82:83], v[82:83], v[114:115] op_sel:[0,1]
	v_mov_b32_e32 v118, v164
	v_pk_fma_f32 v[66:67], v[66:67], v[114:115], v[82:83] op_sel_hi:[1,0,1]
	v_xor_b32_e32 v83, 0x80000000, v44
	v_mov_b32_e32 v82, v45
	v_pk_mul_f32 v[82:83], v[82:83], v[112:113] op_sel:[0,1]
	v_mov_b32_e32 v120, v166
	v_pk_fma_f32 v[44:45], v[44:45], v[112:113], v[82:83] op_sel_hi:[1,0,1]
	v_xor_b32_e32 v83, 0x80000000, v46
	v_mov_b32_e32 v82, v47
	v_pk_mul_f32 v[82:83], v[82:83], v[110:111] op_sel:[0,1]
	v_mov_b32_e32 v122, v168
	v_pk_fma_f32 v[46:47], v[46:47], v[110:111], v[82:83] op_sel_hi:[1,0,1]
	v_xor_b32_e32 v83, 0x80000000, v50
	v_mov_b32_e32 v82, v51
	v_pk_mul_f32 v[82:83], v[82:83], v[108:109] op_sel:[0,1]
	v_mov_b32_e32 v124, v170
	v_pk_fma_f32 v[50:51], v[50:51], v[108:109], v[82:83] op_sel_hi:[1,0,1]
	v_xor_b32_e32 v83, 0x80000000, v54
	v_mov_b32_e32 v82, v55
	v_pk_mul_f32 v[82:83], v[82:83], v[106:107] op_sel:[0,1]
	s_movk_i32 s33, 0x5000
	v_pk_fma_f32 v[54:55], v[54:55], v[106:107], v[82:83] op_sel_hi:[1,0,1]
	v_xor_b32_e32 v83, 0x80000000, v58
	v_mov_b32_e32 v82, v59
	v_pk_mul_f32 v[82:83], v[82:83], v[104:105] op_sel:[0,1]
	s_nop 0
	v_pk_fma_f32 v[58:59], v[58:59], v[104:105], v[82:83] op_sel_hi:[1,0,1]
	v_xor_b32_e32 v83, 0x80000000, v60
	v_mov_b32_e32 v82, v61
	v_pk_mul_f32 v[82:83], v[82:83], v[102:103] op_sel:[0,1]
	s_nop 0
	v_pk_fma_f32 v[60:61], v[60:61], v[102:103], v[82:83] op_sel_hi:[1,0,1]
	v_xor_b32_e32 v83, 0x80000000, v62
	v_mov_b32_e32 v82, v63
	v_pk_mul_f32 v[82:83], v[82:83], v[100:101] op_sel:[0,1]
	s_nop 0
	v_pk_fma_f32 v[62:63], v[62:63], v[100:101], v[82:83] op_sel_hi:[1,0,1]
	v_xor_b32_e32 v83, 0x80000000, v24
	v_mov_b32_e32 v82, v25
	v_pk_mul_f32 v[82:83], v[82:83], v[98:99] op_sel:[0,1]
	s_nop 0
	v_pk_fma_f32 v[24:25], v[24:25], v[98:99], v[82:83] op_sel_hi:[1,0,1]
	v_xor_b32_e32 v83, 0x80000000, v68
	v_mov_b32_e32 v82, v69
	v_pk_mul_f32 v[82:83], v[82:83], v[96:97] op_sel:[0,1]
	v_add_f32_e32 v22, v24, v22
	v_pk_fma_f32 v[68:69], v[68:69], v[96:97], v[82:83] op_sel_hi:[1,0,1]
	v_xor_b32_e32 v83, 0x80000000, v70
	v_mov_b32_e32 v82, v71
	v_pk_mul_f32 v[82:83], v[82:83], v[94:95] op_sel:[0,1]
	v_add_f32_e32 v20, v17, v22
	v_pk_fma_f32 v[70:71], v[70:71], v[94:95], v[82:83] op_sel_hi:[1,0,1]
	v_xor_b32_e32 v83, 0x80000000, v72
	v_mov_b32_e32 v82, v73
	v_pk_mul_f32 v[82:83], v[82:83], v[92:93] op_sel:[0,1]
	v_mov_b32_e32 v94, v170
	v_pk_fma_f32 v[72:73], v[72:73], v[92:93], v[82:83] op_sel_hi:[1,0,1]
	v_xor_b32_e32 v83, 0x80000000, v74
	v_mov_b32_e32 v82, v75
	v_pk_mul_f32 v[82:83], v[82:83], v[90:91] op_sel:[0,1]
	v_mov_b32_e32 v92, v169
	v_pk_fma_f32 v[74:75], v[74:75], v[90:91], v[82:83] op_sel_hi:[1,0,1]
	v_xor_b32_e32 v83, 0x80000000, v76
	v_mov_b32_e32 v82, v77
	v_pk_mul_f32 v[82:83], v[82:83], v[88:89] op_sel:[0,1]
	v_mov_b32_e32 v90, v168
	v_pk_fma_f32 v[76:77], v[76:77], v[88:89], v[82:83] op_sel_hi:[1,0,1]
	v_xor_b32_e32 v83, 0x80000000, v78
	v_mov_b32_e32 v82, v79
	v_pk_mul_f32 v[82:83], v[82:83], v[86:87] op_sel:[0,1]
	v_mov_b32_e32 v88, v167
	v_pk_fma_f32 v[78:79], v[78:79], v[86:87], v[82:83] op_sel_hi:[1,0,1]
	v_xor_b32_e32 v83, 0x80000000, v80
	v_mov_b32_e32 v82, v81
	v_pk_mul_f32 v[82:83], v[84:85], v[82:83] op_sel:[1,0]
	v_mov_b32_e32 v86, v166
	v_pk_fma_f32 v[80:81], v[80:81], v[84:85], v[82:83] op_sel_hi:[1,0,1]
	v_mov_b32_e32 v84, v165
	v_pk_add_f32 v[96:97], v[80:81], v[66:67]
	v_pk_add_f32 v[66:67], v[80:81], v[66:67] neg_lo:[0,1] neg_hi:[0,1]
	s_nop 0
	v_xor_b32_e32 v80, 0x80000000, v67
	v_mov_b32_e32 v81, v66
	v_sub_f32_e32 v82, v25, v23
	v_pk_mul_f32 v[80:81], v[94:95], v[80:81] op_sel_hi:[0,1]
	v_pk_fma_f32 v[80:81], v[10:11], v[66:67], v[80:81] op_sel_hi:[0,1,1]
	v_pk_add_f32 v[66:67], v[78:79], v[64:65]
	v_pk_add_f32 v[64:65], v[78:79], v[64:65] neg_lo:[0,1] neg_hi:[0,1]
	s_nop 0
	v_xor_b32_e32 v78, 0x80000000, v65
	v_mov_b32_e32 v79, v64
	v_pk_mul_f32 v[78:79], v[92:93], v[78:79] op_sel_hi:[0,1]
	v_pk_fma_f32 v[64:65], v[84:85], v[64:65], v[78:79] op_sel_hi:[0,1,1]
	v_pk_add_f32 v[78:79], v[76:77], v[38:39]
	v_pk_add_f32 v[38:39], v[76:77], v[38:39] neg_lo:[0,1] neg_hi:[0,1]
	s_barrier
	v_xor_b32_e32 v76, 0x80000000, v39
	v_mov_b32_e32 v77, v38
	v_pk_mul_f32 v[76:77], v[90:91], v[76:77] op_sel_hi:[0,1]
	v_pk_fma_f32 v[76:77], v[86:87], v[38:39], v[76:77] op_sel_hi:[0,1,1]
	v_pk_add_f32 v[38:39], v[74:75], v[30:31]
	v_pk_add_f32 v[30:31], v[74:75], v[30:31] neg_lo:[0,1] neg_hi:[0,1]
	s_nop 0
	v_xor_b32_e32 v74, 0x80000000, v31
	v_mov_b32_e32 v75, v30
	v_pk_mul_f32 v[74:75], v[88:89], v[74:75] op_sel_hi:[0,1]
	v_pk_fma_f32 v[30:31], v[88:89], v[30:31], v[74:75] op_sel_hi:[0,1,1]
	v_pk_add_f32 v[74:75], v[72:73], v[56:57]
	v_pk_add_f32 v[56:57], v[72:73], v[56:57] neg_lo:[0,1] neg_hi:[0,1]
	v_sub_f32_e32 v22, v17, v22
	v_xor_b32_e32 v72, 0x80000000, v57
	v_mov_b32_e32 v73, v56
	v_pk_mul_f32 v[72:73], v[86:87], v[72:73] op_sel_hi:[0,1]
	v_pk_fma_f32 v[72:73], v[90:91], v[56:57], v[72:73] op_sel_hi:[0,1,1]
	v_pk_add_f32 v[56:57], v[70:71], v[52:53]
	v_pk_add_f32 v[52:53], v[70:71], v[52:53] neg_lo:[0,1] neg_hi:[0,1]
	v_ashrrev_i32_e32 v15, 31, v14
	v_xor_b32_e32 v70, 0x80000000, v53
	v_mov_b32_e32 v71, v52
	v_pk_mul_f32 v[70:71], v[84:85], v[70:71] op_sel_hi:[0,1]
	v_pk_fma_f32 v[52:53], v[92:93], v[52:53], v[70:71] op_sel_hi:[0,1,1]
	v_pk_add_f32 v[70:71], v[68:69], v[48:49]
	v_pk_add_f32 v[48:49], v[68:69], v[48:49] neg_lo:[0,1] neg_hi:[0,1]
	v_lshl_add_u64 v[14:15], v[14:15], 2, s[70:71]
	v_xor_b32_e32 v68, 0x80000000, v49
	v_mov_b32_e32 v69, v48
	v_pk_mul_f32 v[68:69], v[10:11], v[68:69] op_sel_hi:[0,1]
	v_pk_fma_f32 v[98:99], v[94:95], v[48:49], v[68:69] op_sel_hi:[0,1,1]
	v_pk_add_f32 v[48:49], v[62:63], v[42:43]
	v_pk_add_f32 v[42:43], v[62:63], v[42:43] neg_lo:[0,1] neg_hi:[0,1]
	s_nop 0
	v_xor_b32_e32 v62, 0x80000000, v43
	v_mov_b32_e32 v63, v42
	v_pk_mul_f32 v[62:63], v[10:11], v[62:63] op_sel_hi:[0,1]
	v_pk_fma_f32 v[62:63], v[94:95], v[42:43], v[62:63] op_sel_hi:[0,1,1] neg_lo:[1,0,0] neg_hi:[1,0,0]
	v_pk_add_f32 v[42:43], v[60:61], v[40:41]
	v_pk_add_f32 v[40:41], v[60:61], v[40:41] neg_lo:[0,1] neg_hi:[0,1]
	s_nop 0
	v_xor_b32_e32 v60, 0x80000000, v41
	v_mov_b32_e32 v61, v40
	v_pk_mul_f32 v[60:61], v[84:85], v[60:61] op_sel_hi:[0,1]
	v_pk_fma_f32 v[100:101], v[92:93], v[40:41], v[60:61] op_sel_hi:[0,1,1] neg_lo:[1,0,0] neg_hi:[1,0,0]
	v_pk_add_f32 v[60:61], v[58:59], v[36:37]
	v_pk_add_f32 v[36:37], v[58:59], v[36:37] neg_lo:[0,1] neg_hi:[0,1]
	s_nop 0
	v_xor_b32_e32 v40, 0x80000000, v37
	v_mov_b32_e32 v41, v36
	v_pk_mul_f32 v[40:41], v[86:87], v[40:41] op_sel_hi:[0,1]
	v_pk_fma_f32 v[58:59], v[90:91], v[36:37], v[40:41] op_sel_hi:[0,1,1] neg_lo:[1,0,0] neg_hi:[1,0,0]
	v_pk_add_f32 v[40:41], v[54:55], v[34:35]
	v_pk_add_f32 v[34:35], v[54:55], v[34:35] neg_lo:[0,1] neg_hi:[0,1]
	v_pk_add_f32 v[54:55], v[46:47], v[28:29]
	v_xor_b32_e32 v36, 0x80000000, v35
	v_mov_b32_e32 v37, v34
	v_pk_mul_f32 v[36:37], v[88:89], v[36:37] op_sel_hi:[0,1]
	v_pk_fma_f32 v[34:35], v[88:89], v[34:35], v[36:37] op_sel_hi:[0,1,1] neg_lo:[1,0,0] neg_hi:[1,0,0]
	v_pk_add_f32 v[36:37], v[50:51], v[32:33]
	v_pk_add_f32 v[32:33], v[50:51], v[32:33] neg_lo:[0,1] neg_hi:[0,1]
	v_pk_add_f32 v[28:29], v[46:47], v[28:29] neg_lo:[0,1] neg_hi:[0,1]
	v_xor_b32_e32 v50, 0x80000000, v33
	v_mov_b32_e32 v51, v32
	v_pk_mul_f32 v[50:51], v[90:91], v[50:51] op_sel_hi:[0,1]
	v_pk_fma_f32 v[86:87], v[86:87], v[32:33], v[50:51] op_sel_hi:[0,1,1] neg_lo:[1,0,0] neg_hi:[1,0,0]
	v_xor_b32_e32 v32, 0x80000000, v29
	v_mov_b32_e32 v33, v28
	v_pk_mul_f32 v[32:33], v[92:93], v[32:33] op_sel_hi:[0,1]
	v_pk_fma_f32 v[46:47], v[84:85], v[28:29], v[32:33] op_sel_hi:[0,1,1] neg_lo:[1,0,0] neg_hi:[1,0,0]
	v_pk_add_f32 v[28:29], v[44:45], v[26:27]
	v_pk_add_f32 v[26:27], v[44:45], v[26:27] neg_lo:[0,1] neg_hi:[0,1]
	v_pk_add_f32 v[50:51], v[66:67], v[42:43]
	v_xor_b32_e32 v32, 0x80000000, v27
	v_mov_b32_e32 v33, v26
	v_pk_mul_f32 v[32:33], v[94:95], v[32:33] op_sel_hi:[0,1]
	v_pk_fma_f32 v[90:91], v[10:11], v[26:27], v[32:33] op_sel_hi:[0,1,1] neg_lo:[1,0,0] neg_hi:[1,0,0]
	v_pk_add_f32 v[32:33], v[96:97], v[48:49] neg_lo:[0,1] neg_hi:[0,1]
	v_pk_add_f32 v[26:27], v[96:97], v[48:49]
	v_xor_b32_e32 v44, 0x80000000, v33
	v_mov_b32_e32 v45, v32
	v_pk_mul_f32 v[44:45], v[92:93], v[44:45] op_sel_hi:[0,1]
	v_pk_fma_f32 v[48:49], v[84:85], v[32:33], v[44:45] op_sel_hi:[0,1,1]
	v_pk_add_f32 v[32:33], v[66:67], v[42:43] neg_lo:[0,1] neg_hi:[0,1]
	v_pk_add_f32 v[44:45], v[78:79], v[60:61] neg_lo:[0,1] neg_hi:[0,1]
	v_xor_b32_e32 v42, 0x80000000, v33
	v_mov_b32_e32 v43, v32
	v_pk_mul_f32 v[42:43], v[88:89], v[42:43] op_sel_hi:[0,1]
	v_pk_fma_f32 v[32:33], v[88:89], v[32:33], v[42:43] op_sel_hi:[0,1,1]
	v_pk_add_f32 v[42:43], v[78:79], v[60:61]
	v_xor_b32_e32 v60, 0x80000000, v45
	v_mov_b32_e32 v61, v44
	v_pk_mul_f32 v[60:61], v[84:85], v[60:61] op_sel_hi:[0,1]
	v_pk_add_f32 v[78:79], v[74:75], v[36:37]
	v_pk_add_f32 v[36:37], v[74:75], v[36:37] neg_lo:[0,1] neg_hi:[0,1]
	v_pk_fma_f32 v[68:69], v[92:93], v[44:45], v[60:61] op_sel_hi:[0,1,1]
	v_xor_b32_e32 v44, 0x80000000, v37
	v_mov_b32_e32 v45, v36
	v_pk_mul_f32 v[44:45], v[84:85], v[44:45] op_sel_hi:[0,1]
	v_pk_fma_f32 v[74:75], v[92:93], v[36:37], v[44:45] op_sel_hi:[0,1,1] neg_lo:[1,0,0] neg_hi:[1,0,0]
	v_pk_add_f32 v[36:37], v[56:57], v[54:55] neg_lo:[0,1] neg_hi:[0,1]
	v_pk_add_f32 v[60:61], v[56:57], v[54:55]
	v_xor_b32_e32 v44, 0x80000000, v37
	v_mov_b32_e32 v45, v36
	v_pk_mul_f32 v[44:45], v[88:89], v[44:45] op_sel_hi:[0,1]
	v_pk_fma_f32 v[44:45], v[88:89], v[36:37], v[44:45] op_sel_hi:[0,1,1] neg_lo:[1,0,0] neg_hi:[1,0,0]
	v_pk_add_f32 v[36:37], v[70:71], v[28:29]
	v_pk_add_f32 v[28:29], v[70:71], v[28:29] neg_lo:[0,1] neg_hi:[0,1]
	v_pk_add_f32 v[66:67], v[26:27], v[78:79]
	v_xor_b32_e32 v54, 0x80000000, v29
	v_mov_b32_e32 v55, v28
	v_pk_mul_f32 v[54:55], v[92:93], v[54:55] op_sel_hi:[0,1]
	v_pk_add_f32 v[26:27], v[26:27], v[78:79] neg_lo:[0,1] neg_hi:[0,1]
	v_pk_fma_f32 v[94:95], v[84:85], v[28:29], v[54:55] op_sel_hi:[0,1,1] neg_lo:[1,0,0] neg_hi:[1,0,0]
	v_xor_b32_e32 v28, 0x80000000, v27
	v_mov_b32_e32 v29, v26
	v_pk_mul_f32 v[28:29], v[88:89], v[28:29] op_sel_hi:[0,1]
	v_pk_fma_f32 v[26:27], v[88:89], v[26:27], v[28:29] op_sel_hi:[0,1,1]
	v_pk_add_f32 v[28:29], v[42:43], v[36:37] neg_lo:[0,1] neg_hi:[0,1]
	v_pk_add_f32 v[70:71], v[42:43], v[36:37]
	v_xor_b32_e32 v36, 0x80000000, v29
	v_mov_b32_e32 v37, v28
	v_pk_mul_f32 v[36:37], v[88:89], v[36:37] op_sel_hi:[0,1]
	v_pk_fma_f32 v[36:37], v[88:89], v[28:29], v[36:37] op_sel_hi:[0,1,1] neg_lo:[1,0,0] neg_hi:[1,0,0]
	v_pk_add_f32 v[28:29], v[48:49], v[74:75] neg_lo:[0,1] neg_hi:[0,1]
	v_pk_add_f32 v[54:55], v[48:49], v[74:75]
	v_xor_b32_e32 v42, 0x80000000, v29
	v_mov_b32_e32 v43, v28
	v_pk_mul_f32 v[42:43], v[88:89], v[42:43] op_sel_hi:[0,1]
	v_pk_fma_f32 v[28:29], v[88:89], v[28:29], v[42:43] op_sel_hi:[0,1,1]
	v_pk_add_f32 v[42:43], v[68:69], v[94:95] neg_lo:[0,1] neg_hi:[0,1]
	v_pk_add_f32 v[74:75], v[80:81], v[62:63]
	v_xor_b32_e32 v48, 0x80000000, v43
	v_mov_b32_e32 v49, v42
	v_pk_mul_f32 v[48:49], v[88:89], v[48:49] op_sel_hi:[0,1]
	v_pk_fma_f32 v[42:43], v[88:89], v[42:43], v[48:49] op_sel_hi:[0,1,1] neg_lo:[1,0,0] neg_hi:[1,0,0]
	v_pk_add_f32 v[48:49], v[80:81], v[62:63] neg_lo:[0,1] neg_hi:[0,1]
	v_pk_add_f32 v[56:57], v[68:69], v[94:95]
	v_xor_b32_e32 v62, 0x80000000, v49
	v_mov_b32_e32 v63, v48
	v_pk_mul_f32 v[62:63], v[92:93], v[62:63] op_sel_hi:[0,1]
	v_pk_fma_f32 v[94:95], v[84:85], v[48:49], v[62:63] op_sel_hi:[0,1,1]
	v_pk_add_f32 v[48:49], v[64:65], v[100:101] neg_lo:[0,1] neg_hi:[0,1]
	v_pk_add_f32 v[68:69], v[64:65], v[100:101]
	v_xor_b32_e32 v62, 0x80000000, v49
	v_mov_b32_e32 v63, v48
	v_pk_mul_f32 v[62:63], v[88:89], v[62:63] op_sel_hi:[0,1]
	v_pk_add_f32 v[64:65], v[76:77], v[58:59]
	v_pk_add_f32 v[58:59], v[76:77], v[58:59] neg_lo:[0,1] neg_hi:[0,1]
	v_pk_fma_f32 v[48:49], v[88:89], v[48:49], v[62:63] op_sel_hi:[0,1,1]
	v_xor_b32_e32 v62, 0x80000000, v59
	v_mov_b32_e32 v63, v58
	v_pk_mul_f32 v[62:63], v[84:85], v[62:63] op_sel_hi:[0,1]
	v_pk_fma_f32 v[96:97], v[92:93], v[58:59], v[62:63] op_sel_hi:[0,1,1]
	v_pk_add_f32 v[58:59], v[72:73], v[86:87] neg_lo:[0,1] neg_hi:[0,1]
	v_pk_add_f32 v[76:77], v[52:53], v[46:47]
	v_pk_add_f32 v[46:47], v[52:53], v[46:47] neg_lo:[0,1] neg_hi:[0,1]
	v_pk_add_f32 v[62:63], v[72:73], v[86:87]
	v_xor_b32_e32 v72, 0x80000000, v59
	v_mov_b32_e32 v73, v58
	v_xor_b32_e32 v52, 0x80000000, v47
	v_mov_b32_e32 v53, v46
	v_pk_mul_f32 v[72:73], v[84:85], v[72:73] op_sel_hi:[0,1]
	v_pk_mul_f32 v[52:53], v[88:89], v[52:53] op_sel_hi:[0,1]
	v_pk_fma_f32 v[86:87], v[92:93], v[58:59], v[72:73] op_sel_hi:[0,1,1] neg_lo:[1,0,0] neg_hi:[1,0,0]
	v_pk_fma_f32 v[58:59], v[88:89], v[46:47], v[52:53] op_sel_hi:[0,1,1] neg_lo:[1,0,0] neg_hi:[1,0,0]
	v_pk_add_f32 v[46:47], v[98:99], v[90:91]
	v_pk_add_f32 v[52:53], v[98:99], v[90:91] neg_lo:[0,1] neg_hi:[0,1]
	v_pk_add_f32 v[80:81], v[64:65], v[46:47]
	v_pk_add_f32 v[46:47], v[64:65], v[46:47] neg_lo:[0,1] neg_hi:[0,1]
	v_xor_b32_e32 v72, 0x80000000, v53
	v_xor_b32_e32 v64, 0x80000000, v47
	v_mov_b32_e32 v65, v46
	v_pk_mul_f32 v[64:65], v[88:89], v[64:65] op_sel_hi:[0,1]
	v_mov_b32_e32 v73, v52
	v_pk_fma_f32 v[64:65], v[88:89], v[46:47], v[64:65] op_sel_hi:[0,1,1] neg_lo:[1,0,0] neg_hi:[1,0,0]
	v_pk_add_f32 v[46:47], v[94:95], v[86:87] neg_lo:[0,1] neg_hi:[0,1]
	v_pk_mul_f32 v[72:73], v[92:93], v[72:73] op_sel_hi:[0,1]
	v_pk_add_f32 v[78:79], v[74:75], v[62:63]
	v_pk_add_f32 v[62:63], v[74:75], v[62:63] neg_lo:[0,1] neg_hi:[0,1]
	v_xor_b32_e32 v74, 0x80000000, v47
	v_mov_b32_e32 v75, v46
	v_pk_fma_f32 v[52:53], v[84:85], v[52:53], v[72:73] op_sel_hi:[0,1,1] neg_lo:[1,0,0] neg_hi:[1,0,0]
	v_pk_mul_f32 v[74:75], v[88:89], v[74:75] op_sel_hi:[0,1]
	v_pk_fma_f32 v[46:47], v[88:89], v[46:47], v[74:75] op_sel_hi:[0,1,1]
	v_pk_add_f32 v[74:75], v[96:97], v[52:53]
	v_pk_add_f32 v[52:53], v[96:97], v[52:53] neg_lo:[0,1] neg_hi:[0,1]
	v_add_f32_e32 v30, v30, v34
	v_xor_b32_e32 v84, 0x80000000, v53
	v_mov_b32_e32 v85, v52
	v_pk_mul_f32 v[84:85], v[88:89], v[84:85] op_sel_hi:[0,1]
	v_sub_f32_e32 v34, v16, v18
	v_sub_f32_e32 v13, v51, v61
	v_pk_fma_f32 v[52:53], v[88:89], v[52:53], v[84:85] op_sel_hi:[0,1,1] neg_lo:[1,0,0] neg_hi:[1,0,0]
	v_sub_f32_e32 v51, v34, v82
	v_sub_f32_e32 v25, v29, v43
	v_sub_f32_e32 v43, v31, v35
	v_sub_f32_e32 v35, v49, v59
	v_sub_f32_e32 v10, v47, v53
	v_add_f32_e32 v49, v50, v60
	v_add_f32_e32 v50, v68, v76
	v_add_f32_e32 v53, v51, v30
	v_sub_f32_e32 v23, v27, v37
	v_sub_f32_e32 v27, v55, v57
	v_add_f32_e32 v38, v38, v40
	v_add_f32_e32 v40, v78, v80
	v_add_f32_e32 v55, v53, v50
	v_add_f32_e32 v16, v55, v40
	v_sub_f32_e32 v41, v39, v41
	v_add_f32_e32 v21, v20, v38
	global_store_dword v[14:15], v16, off offset:2048
	v_add_co_u32_e32 v16, vcc, s10, v14
	v_xor_b32_e32 v72, 0x80000000, v63
	v_mov_b32_e32 v73, v62
	v_add_f32_e32 v47, v66, v70
	v_add_f32_e32 v24, v21, v49
	v_add_f32_e32 v32, v32, v44
	v_sub_f32_e32 v44, v22, v41
	v_addc_co_u32_e32 v17, vcc, 0, v15, vcc
	v_pk_mul_f32 v[72:73], v[88:89], v[72:73] op_sel_hi:[0,1]
	v_add_f32_e32 v19, v24, v47
	v_add_f32_e32 v54, v54, v56
	v_add_f32_e32 v56, v44, v32
	v_add_co_u32_e32 v18, vcc, s11, v14
	v_add_f32_e32 v34, v34, v82
	v_pk_fma_f32 v[62:63], v[88:89], v[62:63], v[72:73] op_sel_hi:[0,1,1]
	v_pk_add_f32 v[72:73], v[94:95], v[86:87]
	global_store_dword v[14:15], v19, off
	v_add_f32_e32 v57, v56, v54
	v_addc_co_u32_e32 v19, vcc, 0, v15, vcc
	v_add_f32_e32 v48, v48, v58
	v_sub_f32_e32 v58, v34, v43
	global_store_dword v[18:19], v57, off offset:-4096
	v_add_f32_e32 v57, v72, v74
	v_add_f32_e32 v59, v58, v48
	v_sub_f32_e32 v20, v20, v38
	v_sub_f32_e32 v37, v33, v45
	v_sub_f32_e32 v45, v69, v77
	v_add_f32_e32 v60, v59, v57
	v_add_f32_e32 v26, v26, v36
	v_sub_f32_e32 v36, v20, v13
	v_sub_f32_e32 v30, v51, v30
	global_store_dword v[16:17], v60, off offset:2048
	v_add_f32_e32 v16, v36, v26
	v_add_f32_e32 v38, v62, v64
	v_sub_f32_e32 v51, v30, v45
	global_store_dword v[18:19], v16, off
	v_add_f32_e32 v16, v51, v38
	global_store_dword v[18:19], v16, off offset:2048
	v_add_co_u32_e32 v16, vcc, s78, v14
	v_add_f32_e32 v22, v22, v41
	s_nop 0
	v_addc_co_u32_e32 v17, vcc, 0, v15, vcc
	v_add_f32_e32 v28, v28, v42
	v_sub_f32_e32 v41, v22, v37
	v_add_co_u32_e32 v18, vcc, s43, v14
	v_add_f32_e32 v42, v41, v28
	s_nop 0
	v_addc_co_u32_e32 v19, vcc, 0, v15, vcc
	v_add_f32_e32 v34, v34, v43
	global_store_dword v[18:19], v42, off offset:-4096
	v_add_f32_e32 v42, v46, v52
	v_sub_f32_e32 v43, v34, v35
	v_sub_f32_e32 v39, v67, v71
	v_add_f32_e32 v46, v43, v42
	v_sub_f32_e32 v21, v21, v49
	v_sub_f32_e32 v33, v79, v81
	global_store_dword v[16:17], v46, off offset:2048
	v_sub_f32_e32 v16, v21, v39
	v_sub_f32_e32 v46, v53, v50
	global_store_dword v[18:19], v16, off
	v_sub_f32_e32 v16, v46, v33
	global_store_dword v[18:19], v16, off offset:2048
	v_add_co_u32_e32 v16, vcc, s13, v14
	v_sub_f32_e32 v32, v44, v32
	s_nop 0
	v_addc_co_u32_e32 v17, vcc, 0, v15, vcc
	v_add_co_u32_e32 v18, vcc, s12, v14
	v_sub_f32_e32 v44, v32, v27
	s_nop 0
	v_addc_co_u32_e32 v19, vcc, 0, v15, vcc
	v_sub_f32_e32 v31, v73, v75
	global_store_dword v[18:19], v44, off offset:-4096
	v_sub_f32_e32 v44, v58, v48
	v_sub_f32_e32 v48, v44, v31
	v_add_f32_e32 v20, v20, v13
	v_sub_f32_e32 v29, v63, v65
	global_store_dword v[16:17], v48, off offset:2048
	v_sub_f32_e32 v13, v20, v23
	v_add_f32_e32 v30, v30, v45
	v_add_co_u32_e32 v16, vcc, s16, v14
	global_store_dword v[18:19], v13, off
	v_sub_f32_e32 v13, v30, v29
	v_addc_co_u32_e32 v17, vcc, 0, v15, vcc
	global_store_dword v[18:19], v13, off offset:2048
	v_add_f32_e32 v22, v22, v37
	v_add_co_u32_e32 v18, vcc, s8, v14
	v_sub_f32_e32 v13, v22, v25
	s_nop 0
	v_addc_co_u32_e32 v19, vcc, 0, v15, vcc
	global_store_dword v[18:19], v13, off offset:-4096
	v_add_f32_e32 v13, v34, v35
	v_sub_f32_e32 v34, v13, v10
	global_store_dword v[16:17], v34, off offset:2048
	v_sub_f32_e32 v16, v24, v47
	global_store_dword v[18:19], v16, off
	v_sub_f32_e32 v16, v55, v40
	global_store_dword v[18:19], v16, off offset:2048
	v_add_co_u32_e32 v16, vcc, s9, v14
	v_sub_f32_e32 v24, v56, v54
	s_nop 0
	v_addc_co_u32_e32 v17, vcc, 0, v15, vcc
	v_add_co_u32_e32 v18, vcc, s7, v14
	v_add_f32_e32 v10, v13, v10
	s_nop 0
	v_addc_co_u32_e32 v19, vcc, 0, v15, vcc
	global_store_dword v[18:19], v24, off offset:-4096
	v_sub_f32_e32 v24, v59, v57
	global_store_dword v[16:17], v24, off offset:2048
	v_sub_f32_e32 v16, v36, v26
	global_store_dword v[18:19], v16, off
	v_sub_f32_e32 v16, v51, v38
	global_store_dword v[18:19], v16, off offset:2048
	v_add_co_u32_e32 v16, vcc, s5, v14
	v_sub_f32_e32 v24, v41, v28
	s_nop 0
	v_addc_co_u32_e32 v17, vcc, 0, v15, vcc
	v_add_co_u32_e32 v18, vcc, s6, v14
	s_nop 1
	v_addc_co_u32_e32 v19, vcc, 0, v15, vcc
	global_store_dword v[18:19], v24, off offset:-4096
	v_sub_f32_e32 v24, v43, v42
	global_store_dword v[16:17], v24, off offset:2048
	v_add_f32_e32 v16, v21, v39
	global_store_dword v[18:19], v16, off
	v_add_f32_e32 v16, v46, v33
	global_store_dword v[18:19], v16, off offset:2048
	v_add_co_u32_e32 v16, vcc, s4, v14
	v_add_f32_e32 v21, v32, v27
	s_nop 0
	v_addc_co_u32_e32 v17, vcc, 0, v15, vcc
	v_add_co_u32_e32 v18, vcc, s1, v14
	s_nop 1
	v_addc_co_u32_e32 v19, vcc, 0, v15, vcc
	global_store_dword v[18:19], v21, off offset:-4096
	v_add_f32_e32 v21, v44, v31
	global_store_dword v[16:17], v21, off offset:2048
	v_add_f32_e32 v16, v20, v23
	global_store_dword v[18:19], v16, off
	v_add_f32_e32 v16, v30, v29
	v_add_co_u32_e32 v14, vcc, s0, v14
	global_store_dword v[18:19], v16, off offset:2048
	v_add_f32_e32 v16, v22, v25
	v_addc_co_u32_e32 v15, vcc, 0, v15, vcc
	global_store_dword v[14:15], v16, off
	global_store_dword v[14:15], v10, off offset:2048
	v_mov_b32_e32 v10, v183
	v_mov_b32_e32 v14, v184
	v_mov_b32_e32 v18, v182
	s_movk_i32 s0, 0xfe00
	v_sub_u32_e32 v13, 0x4000, v18
	v_cmp_eq_u32_e32 vcc, 0, v18
	v_cmp_eq_u32_e64 s[0:1], s0, v18
	v_cmp_eq_u32_e64 s[4:5], s48, v18
	v_cndmask_b32_e64 v20, v13, 0, vcc
	v_sub_u32_e32 v13, 0x3e00, v18
	v_cndmask_b32_e64 v22, v13, 0, s[0:1]
	v_sub_u32_e32 v13, 0x3c00, v18
	v_ashrrev_i32_e32 v21, 31, v20
	v_ashrrev_i32_e32 v23, 31, v22
	v_cndmask_b32_e64 v24, v13, 0, s[4:5]
	v_lshl_add_u64 v[20:21], v[20:21], 1, s[2:3]
	v_lshl_add_u64 v[22:23], v[22:23], 1, s[2:3]
	v_ashrrev_i32_e32 v25, 31, v24
	v_sub_u32_e32 v13, 0x3a00, v18
	v_cmp_eq_u32_e64 s[6:7], s49, v18
	v_lshl_add_u64 v[24:25], v[24:25], 1, s[2:3]
	global_load_ushort v15, v[20:21], off
	s_nop 0
	global_load_ushort v22, v[22:23], off
	s_nop 0
	global_load_ushort v23, v[24:25], off
	v_cndmask_b32_e64 v20, v13, 0, s[6:7]
	v_ashrrev_i32_e32 v21, 31, v20
	v_ashrrev_i32_e32 v19, 31, v18
	v_lshl_add_u64 v[20:21], v[20:21], 1, s[2:3]
	v_lshl_add_u64 v[16:17], v[18:19], 1, s[76:77]
	global_load_ushort v20, v[20:21], off
	s_nop 0
	global_load_ushort v13, v[16:17], off offset:3072
	v_sub_u32_e32 v24, 0x3800, v18
	v_sub_u32_e32 v26, 0x3600, v18
	v_sub_u32_e32 v28, 0x3400, v18
	v_sub_u32_e32 v32, 0x3200, v18
	v_cmp_eq_u32_e64 s[8:9], s59, v18
	s_mov_b32 s48, s21
	s_mov_b32 s49, s20
	s_mov_b32 s59, s82
	s_waitcnt vmcnt(4)
	v_lshlrev_b32_e32 v15, 16, v15
	v_cndmask_b32_e64 v19, -v15, v15, vcc
	s_waitcnt vmcnt(3)
	v_lshlrev_b32_e32 v15, 16, v22
	v_cndmask_b32_e64 v31, -v15, v15, s[0:1]
	s_waitcnt vmcnt(2)
	v_lshlrev_b32_e32 v15, 16, v23
	v_cndmask_b32_e64 v30, -v15, v15, s[4:5]
	v_cmp_eq_u32_e64 s[4:5], s51, v18
	s_waitcnt vmcnt(1)
	v_lshlrev_b32_e32 v15, 16, v20
	v_add_co_u32_e32 v20, vcc, s10, v16
	v_cndmask_b32_e64 v15, -v15, v15, s[6:7]
	s_nop 0
	v_addc_co_u32_e32 v21, vcc, 0, v17, vcc
	v_add_co_u32_e32 v22, vcc, s11, v16
	v_cmp_eq_u32_e64 s[6:7], s50, v18
	s_nop 0
	v_addc_co_u32_e32 v23, vcc, 0, v17, vcc
	v_cmp_eq_u32_e64 s[0:1], s57, v18
	v_cndmask_b32_e64 v24, v24, 0, s[6:7]
	v_cndmask_b32_e64 v26, v26, 0, s[4:5]
	v_cndmask_b32_e64 v28, v28, 0, s[0:1]
	v_cmp_eq_u32_e32 vcc, s58, v18
	v_ashrrev_i32_e32 v25, 31, v24
	v_ashrrev_i32_e32 v27, 31, v26
	v_ashrrev_i32_e32 v29, 31, v28
	v_cndmask_b32_e64 v32, v32, 0, vcc
	v_lshl_add_u64 v[24:25], v[24:25], 1, s[2:3]
	v_lshl_add_u64 v[26:27], v[26:27], 1, s[2:3]
	v_lshl_add_u64 v[28:29], v[28:29], 1, s[2:3]
	v_ashrrev_i32_e32 v33, 31, v32
	v_lshl_add_u64 v[32:33], v[32:33], 1, s[2:3]
	global_load_ushort v34, v[24:25], off
	s_nop 0
	global_load_ushort v26, v[26:27], off
	s_nop 0
	global_load_ushort v27, v[28:29], off
	s_nop 0
	global_load_ushort v28, v[32:33], off
	v_sub_u32_e32 v24, 0x3000, v18
	v_cndmask_b32_e64 v24, v24, 0, s[8:9]
	v_ashrrev_i32_e32 v25, 31, v24
	v_lshl_add_u64 v[24:25], v[24:25], 1, s[2:3]
	global_load_ushort v24, v[24:25], off
	s_nop 0
	global_load_ushort v32, v[20:21], off offset:3072
	v_cmp_eq_u32_e64 s[10:11], s79, v18
	s_mov_b32 s79, s80
	s_waitcnt vmcnt(6)
	v_lshlrev_b32_e32 v13, 16, v13
	s_mov_b32 s57, s18
	s_mov_b32 s58, s83
	s_waitcnt vmcnt(5)
	v_lshlrev_b32_e32 v25, 16, v34
	v_cndmask_b32_e64 v33, -v25, v25, s[6:7]
	s_waitcnt vmcnt(4)
	v_lshlrev_b32_e32 v25, 16, v26
	v_cndmask_b32_e64 v34, -v25, v25, s[4:5]
	s_waitcnt vmcnt(3)
	v_lshlrev_b32_e32 v25, 16, v27
	v_cndmask_b32_e64 v35, -v25, v25, s[0:1]
	v_add_co_u32_e64 v26, s[0:1], s78, v16
	s_waitcnt vmcnt(2)
	v_lshlrev_b32_e32 v25, 16, v28
	s_waitcnt vmcnt(1)
	v_lshlrev_b32_e32 v24, 16, v24
	v_addc_co_u32_e64 v27, s[0:1], 0, v17, s[0:1]
	v_cndmask_b32_e64 v36, -v25, v25, vcc
	v_cndmask_b32_e64 v37, -v24, v24, s[8:9]
	v_sub_u32_e32 v24, 0x2e00, v18
	v_cmp_eq_u32_e32 vcc, s60, v18
	v_sub_u32_e32 v28, 0x2c00, v18
	v_cmp_eq_u32_e64 s[0:1], s61, v18
	v_cndmask_b32_e64 v24, v24, 0, vcc
	v_ashrrev_i32_e32 v25, 31, v24
	v_cndmask_b32_e64 v28, v28, 0, s[0:1]
	v_ashrrev_i32_e32 v29, 31, v28
	v_lshl_add_u64 v[24:25], v[24:25], 1, s[2:3]
	v_lshl_add_u64 v[28:29], v[28:29], 1, s[2:3]
	global_load_ushort v41, v[24:25], off
	s_nop 0
	global_load_ushort v28, v[28:29], off
	v_sub_u32_e32 v24, 0x2a00, v18
	v_cmp_eq_u32_e64 s[4:5], s62, v18
	v_cmp_eq_u32_e64 s[6:7], s63, v18
	v_cmp_eq_u32_e64 s[8:9], s68, v18
	v_cndmask_b32_e64 v24, v24, 0, s[4:5]
	v_ashrrev_i32_e32 v25, 31, v24
	v_lshl_add_u64 v[24:25], v[24:25], 1, s[2:3]
	global_load_ushort v29, v[24:25], off
	v_sub_u32_e32 v24, 0x2800, v18
	v_cndmask_b32_e64 v24, v24, 0, s[6:7]
	v_ashrrev_i32_e32 v25, 31, v24
	v_lshl_add_u64 v[24:25], v[24:25], 1, s[2:3]
	global_load_ushort v38, v[26:27], off offset:1024
	global_load_ushort v40, v[26:27], off offset:2048
	global_load_ushort v39, v[26:27], off offset:3072
	global_load_ushort v44, v[24:25], off
	v_sub_u32_e32 v26, 0x2600, v18
	s_mov_b32 s78, s81
	s_mov_b32 s60, s87
	s_mov_b32 s61, s86
	s_mov_b32 s68, s89
	s_mov_b32 s62, s93
	s_mov_b32 s63, s92
	s_waitcnt vmcnt(6)
	v_lshlrev_b32_e32 v24, 16, v41
	v_cndmask_b32_e64 v43, -v24, v24, vcc
	s_waitcnt vmcnt(5)
	v_lshlrev_b32_e32 v24, 16, v28
	v_cndmask_b32_e64 v41, -v24, v24, s[0:1]
	v_add_co_u32_e64 v28, s[0:1], s13, v16
	s_waitcnt vmcnt(4)
	v_lshlrev_b32_e32 v24, 16, v29
	v_cndmask_b32_e64 v42, -v24, v24, s[4:5]
	v_add_co_u32_e32 v24, vcc, s43, v16
	v_addc_co_u32_e64 v29, s[0:1], 0, v17, s[0:1]
	s_nop 0
	v_addc_co_u32_e32 v25, vcc, 0, v17, vcc
	v_cmp_eq_u32_e32 vcc, s66, v18
	v_cmp_eq_u32_e64 s[4:5], s74, v18
	v_cmp_eq_u32_e64 s[0:1], s75, v18
	v_cndmask_b32_e64 v26, v26, 0, vcc
	v_ashrrev_i32_e32 v27, 31, v26
	v_lshl_add_u64 v[26:27], v[26:27], 1, s[2:3]
	global_load_ushort v26, v[26:27], off
	s_waitcnt vmcnt(1)
	v_lshlrev_b32_e32 v27, 16, v44
	v_sub_u32_e32 v44, 0x2200, v18
	v_cndmask_b32_e64 v45, -v27, v27, s[6:7]
	v_cndmask_b32_e64 v46, v44, 0, s[8:9]
	v_sub_u32_e32 v44, 0x2000, v18
	v_cmp_eq_u32_e64 s[6:7], s69, v18
	v_ashrrev_i32_e32 v47, 31, v46
	v_lshl_add_u64 v[46:47], v[46:47], 1, s[2:3]
	v_cndmask_b32_e64 v50, v44, 0, s[6:7]
	v_sub_u32_e32 v44, 0x1e00, v18
	v_cndmask_b32_e64 v52, v44, 0, s[4:5]
	v_sub_u32_e32 v44, 0x1c00, v18
	v_ashrrev_i32_e32 v51, 31, v50
	v_cndmask_b32_e64 v54, v44, 0, s[0:1]
	v_lshl_add_u64 v[50:51], v[50:51], 1, s[2:3]
	v_ashrrev_i32_e32 v53, 31, v52
	v_ashrrev_i32_e32 v55, 31, v54
	v_lshl_add_u64 v[52:53], v[52:53], 1, s[2:3]
	v_lshl_add_u64 v[54:55], v[54:55], 1, s[2:3]
	s_mov_b32 s66, s25
	s_mov_b32 s69, s88
	s_mov_b32 s74, s29
	s_mov_b32 s75, s28
	s_movk_i32 s43, 0x6000
	s_waitcnt vmcnt(0)
	v_lshlrev_b32_e32 v26, 16, v26
	v_cndmask_b32_e64 v49, -v26, v26, vcc
	v_sub_u32_e32 v26, 0x2400, v18
	v_cmp_eq_u32_e32 vcc, s67, v18
	s_mov_b32 s67, s24
	s_nop 0
	v_cndmask_b32_e64 v26, v26, 0, vcc
	v_ashrrev_i32_e32 v27, 31, v26
	v_lshl_add_u64 v[26:27], v[26:27], 1, s[2:3]
	global_load_ushort v44, v[26:27], off
	s_nop 0
	global_load_ushort v46, v[46:47], off
	s_nop 0
	global_load_ushort v47, v[50:51], off
	global_load_ushort v48, v[52:53], off
	s_nop 0
	global_load_ushort v50, v[54:55], off
	v_sub_u32_e32 v26, 0x1a00, v18
	v_cndmask_b32_e64 v26, v26, 0, s[10:11]
	v_ashrrev_i32_e32 v27, 31, v26
	v_lshl_add_u64 v[26:27], v[26:27], 1, s[2:3]
	global_load_ushort v26, v[26:27], off
	s_nop 0
	global_load_ushort v53, v[28:29], off offset:1024
	global_load_ushort v51, v[28:29], off offset:2048
	s_waitcnt vmcnt(7)
	v_lshlrev_b32_e32 v27, 16, v44
	v_cndmask_b32_e64 v61, -v27, v27, vcc
	s_waitcnt vmcnt(6)
	v_lshlrev_b32_e32 v27, 16, v46
	v_cndmask_b32_e64 v63, -v27, v27, s[8:9]
	s_waitcnt vmcnt(5)
	v_lshlrev_b32_e32 v27, 16, v47
	v_cndmask_b32_e64 v90, -v27, v27, s[6:7]
	s_waitcnt vmcnt(4)
	v_lshlrev_b32_e32 v27, 16, v48
	v_cndmask_b32_e64 v59, -v27, v27, s[4:5]
	s_waitcnt vmcnt(3)
	v_lshlrev_b32_e32 v27, 16, v50
	v_cndmask_b32_e64 v57, -v27, v27, s[0:1]
	v_sub_u32_e32 v44, 0x1800, v18
	v_cmp_eq_u32_e64 s[8:9], s56, v18
	s_movk_i32 s0, 0xd600
	s_waitcnt vmcnt(2)
	v_lshlrev_b32_e32 v26, 16, v26
	v_cndmask_b32_e64 v46, v44, 0, s[8:9]
	v_sub_u32_e32 v44, 0x1600, v18
	v_cmp_eq_u32_e64 s[6:7], s0, v18
	s_movk_i32 s0, 0xd400
	v_cndmask_b32_e64 v55, -v26, v26, s[10:11]
	v_add_co_u32_e32 v26, vcc, s12, v16
	v_cndmask_b32_e64 v64, v44, 0, s[6:7]
	v_sub_u32_e32 v44, 0x1400, v18
	v_cmp_eq_u32_e64 s[4:5], s0, v18
	s_movk_i32 s0, 0xd200
	v_addc_co_u32_e32 v27, vcc, 0, v17, vcc
	v_cndmask_b32_e64 v66, v44, 0, s[4:5]
	v_sub_u32_e32 v44, 0x1200, v18
	v_cmp_eq_u32_e64 s[0:1], s0, v18
	s_movk_i32 s10, 0xd000
	v_cmp_eq_u32_e32 vcc, s10, v18
	v_cndmask_b32_e64 v68, v44, 0, s[0:1]
	v_sub_u32_e32 v44, 0x1000, v18
	v_ashrrev_i32_e32 v47, 31, v46
	v_cndmask_b32_e64 v70, v44, 0, vcc
	v_lshl_add_u64 v[46:47], v[46:47], 1, s[2:3]
	v_ashrrev_i32_e32 v65, 31, v64
	v_ashrrev_i32_e32 v67, 31, v66
	v_ashrrev_i32_e32 v69, 31, v68
	v_ashrrev_i32_e32 v71, 31, v70
	v_lshl_add_u64 v[64:65], v[64:65], 1, s[2:3]
	v_lshl_add_u64 v[66:67], v[66:67], 1, s[2:3]
	v_lshl_add_u64 v[68:69], v[68:69], 1, s[2:3]
	v_lshl_add_u64 v[70:71], v[70:71], 1, s[2:3]
	global_load_ushort v44, v[46:47], off
	global_load_ushort v48, v[64:65], off
	global_load_ushort v50, v[66:67], off
	global_load_ushort v52, v[68:69], off
	global_load_ushort v54, v[70:71], off
	v_sub_u32_e32 v46, 0xe00, v18
	v_cmp_eq_u32_e64 s[12:13], s84, v18
	s_movk_i32 s10, 0xcc00
	v_cmp_eq_u32_e64 s[10:11], s10, v18
	v_cndmask_b32_e64 v46, v46, 0, s[12:13]
	v_ashrrev_i32_e32 v47, 31, v46
	v_lshl_add_u64 v[46:47], v[46:47], 1, s[2:3]
	global_load_ushort v56, v[46:47], off
	v_sub_u32_e32 v46, 0xc00, v18
	v_cndmask_b32_e64 v46, v46, 0, s[10:11]
	v_ashrrev_i32_e32 v47, 31, v46
	v_lshl_add_u64 v[46:47], v[46:47], 1, s[2:3]
	global_load_ushort v46, v[46:47], off
	s_nop 0
	global_load_ushort v91, v[28:29], off offset:3072
	s_mov_b32 s84, 0x3f3504f3
	s_mov_b32 s85, 0xbf3504f3
	s_mov_b32 s54, s85
	s_mov_b32 s55, s84
	s_mov_b32 s56, s19
	s_mov_b32 s38, s85
	s_waitcnt vmcnt(7)
	v_lshlrev_b32_e32 v28, 16, v44
	v_cndmask_b32_e64 v97, -v28, v28, s[8:9]
	s_waitcnt vmcnt(6)
	v_lshlrev_b32_e32 v28, 16, v48
	v_cndmask_b32_e64 v96, -v28, v28, s[6:7]
	s_waitcnt vmcnt(5)
	v_lshlrev_b32_e32 v28, 16, v50
	v_cndmask_b32_e64 v94, -v28, v28, s[4:5]
	s_waitcnt vmcnt(4)
	v_lshlrev_b32_e32 v28, 16, v52
	v_cndmask_b32_e64 v93, -v28, v28, s[0:1]
	s_waitcnt vmcnt(3)
	v_lshlrev_b32_e32 v28, 16, v54
	v_cndmask_b32_e64 v92, -v28, v28, vcc
	s_movk_i32 s0, 0xca00
	v_cmp_eq_u32_e64 s[0:1], s0, v18
	s_waitcnt vmcnt(2)
	v_lshlrev_b32_e32 v28, 16, v56
	v_cndmask_b32_e64 v95, -v28, v28, s[12:13]
	v_sub_u32_e32 v28, 0xa00, v18
	v_cndmask_b32_e64 v28, v28, 0, s[0:1]
	v_ashrrev_i32_e32 v29, 31, v28
	v_lshl_add_u64 v[28:29], v[28:29], 1, s[2:3]
	global_load_ushort v44, v[28:29], off
	s_waitcnt vmcnt(2)
	v_lshlrev_b32_e32 v28, 16, v46
	v_cndmask_b32_e64 v106, -v28, v28, s[10:11]
	v_add_co_u32_e32 v28, vcc, s16, v16
	s_movk_i32 s4, 0xc400
	s_nop 0
	v_addc_co_u32_e32 v29, vcc, 0, v17, vcc
	v_sub_u32_e32 v46, 0x400, v18
	v_cmp_eq_u32_e32 vcc, s4, v18
	s_movk_i32 s4, 0xc800
	v_sub_u32_e32 v48, 0x800, v18
	v_cndmask_b32_e64 v46, v46, 0, vcc
	v_cmp_eq_u32_e64 s[4:5], s4, v18
	v_ashrrev_i32_e32 v47, 31, v46
	v_lshl_add_u64 v[46:47], v[46:47], 1, s[2:3]
	v_cndmask_b32_e64 v64, v48, 0, s[4:5]
	v_ashrrev_i32_e32 v65, 31, v64
	v_lshl_add_u64 v[64:65], v[64:65], 1, s[2:3]
	global_load_ushort v48, v[46:47], off
	s_nop 0
	global_load_ushort v46, v[64:65], off
	global_load_ushort v110, v[28:29], off
	global_load_ushort v112, v[28:29], off offset:1024
	global_load_ushort v114, v[28:29], off offset:2048
	global_load_ushort v116, v[28:29], off offset:3072
	s_mov_b32 s6, 0x3f7b14be
	s_mov_b32 s7, 0xbe47c5c2
	s_mov_b32 s16, 0x3f6c835e
	s_mov_b32 s17, 0xbec3ef15
	s_mov_b32 s50, s17
	s_mov_b32 s51, s16
	v_add_f32_e32 v50, v15, v13
	s_mov_b32 s8, 0x3e47c5c2
	s_mov_b32 s9, 0xbf7b14be
	s_mov_b32 s30, s9
	s_mov_b32 s31, s8
	s_mov_b32 s10, s93
	s_mov_b32 s11, s81
	s_mov_b32 s12, s17
	s_mov_b32 s13, s19
	s_waitcnt vmcnt(6)
	v_lshlrev_b32_e32 v28, 16, v44
	v_cndmask_b32_e64 v108, -v28, v28, s[0:1]
	s_movk_i32 s0, 0xc600
	v_sub_u32_e32 v28, 0x600, v18
	v_sub_u32_e32 v44, 0x200, v18
	s_waitcnt vmcnt(4)
	v_lshlrev_b32_e32 v29, 16, v46
	v_cndmask_b32_e64 v111, -v29, v29, s[4:5]
	v_cmp_eq_u32_e64 s[4:5], s0, v18
	s_movk_i32 s0, 0xc200
	v_cmp_eq_u32_e64 s[0:1], s0, v18
	v_cndmask_b32_e64 v28, v28, 0, s[4:5]
	v_ashrrev_i32_e32 v29, 31, v28
	v_cndmask_b32_e64 v46, v44, 0, s[0:1]
	v_lshl_add_u64 v[28:29], v[28:29], 1, s[2:3]
	v_ashrrev_i32_e32 v47, 31, v46
	v_lshl_add_u64 v[46:47], v[46:47], 1, s[2:3]
	global_load_ushort v18, v[16:17], off
	s_nop 0
	global_load_ushort v28, v[28:29], off
	s_nop 0
	global_load_ushort v29, v[16:17], off offset:1024
	s_nop 0
	global_load_ushort v17, v[16:17], off offset:2048
	s_nop 0
	global_load_ushort v44, v[46:47], off
	global_load_ushort v58, v[22:23], off offset:1024
	global_load_ushort v62, v[22:23], off offset:2048
	global_load_ushort v68, v[22:23], off offset:3072
	global_load_ushort v69, v[24:25], off offset:-4096
	global_load_ushort v98, v[24:25], off
	global_load_ushort v52, v[22:23], off offset:-4096
	global_load_ushort v54, v[20:21], off offset:1024
	s_nop 0
	global_load_ushort v21, v[20:21], off offset:2048
	s_nop 0
	global_load_ushort v56, v[22:23], off
	s_mov_b32 s2, 0x3f7ec46d
	s_mov_b32 s3, 0xbdc8bd36
	v_lshlrev_b32_e32 v22, 16, v48
	s_mov_b32 s76, s3
	s_mov_b32 s77, s2
	v_cndmask_b32_e64 v115, -v22, v22, vcc
	v_pk_mul_f32 v[22:23], v[14:15], s[76:77] op_sel_hi:[0,1] neg_lo:[1,0]
	s_mov_b64 vcc, s[64:65]
	s_mov_b32 s64, s7
	s_mov_b32 s65, s6
	s_waitcnt vmcnt(13)
	v_lshlrev_b32_e32 v16, 16, v18
	s_waitcnt vmcnt(12)
	v_lshlrev_b32_e32 v18, 16, v28
	s_waitcnt vmcnt(11)
	v_lshlrev_b32_e32 v20, 16, v29
	s_waitcnt vmcnt(10)
	v_lshlrev_b32_e32 v17, 16, v17
	v_add_f32_e32 v20, v31, v20
	v_pk_fma_f32 v[28:29], v[10:11], s[2:3], v[22:23] op_sel_hi:[0,1,1]
	v_add_f32_e32 v22, v30, v17
	v_pk_mul_f32 v[30:31], v[14:15], s[64:65] op_sel_hi:[0,1] neg_lo:[1,0]
	v_pk_fma_f32 v[46:47], v[10:11], s[6:7], v[30:31] op_sel_hi:[0,1,1]
	v_pk_mul_f32 v[30:31], v[14:15], s[78:79] op_sel_hi:[0,1] neg_lo:[1,0]
	v_pk_fma_f32 v[88:89], v[10:11], s[80:81], v[30:31] op_sel_hi:[0,1,1]
	s_waitcnt vmcnt(3)
	v_lshlrev_b32_e32 v13, 16, v52
	v_pk_mul_f32 v[30:31], v[14:15], s[50:51] op_sel_hi:[0,1] neg_lo:[1,0]
	v_add_f32_e32 v16, v19, v16
	v_cndmask_b32_e64 v113, -v18, v18, s[4:5]
	v_pk_mul_f32 v[18:19], v[14:15], s[40:41] op_sel_hi:[0,1] neg_lo:[1,0]
	v_add_f32_e32 v52, v33, v13
	v_pk_fma_f32 v[84:85], v[10:11], s[16:17], v[30:31] op_sel_hi:[0,1,1]
	s_waitcnt vmcnt(2)
	v_lshlrev_b32_e32 v13, 16, v54
	v_pk_mul_f32 v[30:31], v[14:15], s[48:49] op_sel_hi:[0,1] neg_lo:[1,0]
	s_waitcnt vmcnt(1)
	v_lshlrev_b32_e32 v15, 16, v21
	v_lshlrev_b32_e32 v17, 16, v44
	v_add_f32_e32 v44, v34, v13
	global_load_ushort v13, v[24:25], off offset:1024
	global_load_ushort v33, v[26:27], off
	v_add_f32_e32 v48, v35, v15
	global_load_ushort v15, v[24:25], off offset:2048
	v_lshlrev_b32_e32 v21, 16, v32
	s_waitcnt vmcnt(3)
	v_lshlrev_b32_e32 v23, 16, v56
	v_add_f32_e32 v54, v36, v21
	global_load_ushort v21, v[24:25], off offset:3072
	v_add_f32_e32 v56, v37, v23
	v_lshlrev_b32_e32 v23, 16, v58
	v_add_f32_e32 v60, v43, v23
	global_load_ushort v23, v[26:27], off offset:-4096
	v_pk_fma_f32 v[64:65], v[10:11], s[20:21], v[30:31] op_sel_hi:[0,1,1]
	s_mov_b32 s4, 0x3dc8bd36
	s_mov_b32 s5, 0xbf7ec46d
	s_mov_b32 s34, s5
	s_mov_b32 s35, s4
	s_mov_b32 s2, s5
	v_cndmask_b32_e64 v17, -v17, v17, s[0:1]
	s_mov_b32 s0, s3
	s_mov_b32 s1, s5
	s_mov_b32 s6, s9
	s_mov_b32 s16, s19
	s_mov_b32 s20, s89
	v_pk_fma_f32 v[18:19], v[10:11], s[44:45], v[18:19] op_sel_hi:[0,1,1]
	s_waitcnt vmcnt(4)
	v_lshlrev_b32_e32 v13, 16, v13
	s_waitcnt vmcnt(2)
	v_pk_mul_f32 v[24:25], v[14:15], s[54:55] op_sel_hi:[0,1] neg_lo:[1,0]
	v_pk_fma_f32 v[78:79], v[10:11], s[84:85], v[24:25] op_sel_hi:[0,1,1]
	v_pk_mul_f32 v[24:25], v[14:15], s[60:61] op_sel_hi:[0,1] neg_lo:[1,0]
	v_pk_fma_f32 v[86:87], v[10:11], s[86:87], v[24:25] op_sel_hi:[0,1,1]
	v_lshlrev_b32_e32 v24, 16, v62
	v_add_f32_e32 v62, v41, v24
	v_pk_mul_f32 v[24:25], v[14:15], s[66:67] op_sel_hi:[0,1] neg_lo:[1,0]
	v_pk_fma_f32 v[82:83], v[10:11], s[24:25], v[24:25] op_sel_hi:[0,1,1]
	v_lshlrev_b32_e32 v24, 16, v68
	v_add_f32_e32 v58, v42, v24
	v_pk_mul_f32 v[24:25], v[14:15], s[68:69] op_sel_hi:[0,1] neg_lo:[1,0]
	v_pk_fma_f32 v[80:81], v[10:11], s[88:89], v[24:25] op_sel_hi:[0,1,1]
	v_lshlrev_b32_e32 v24, 16, v69
	v_add_f32_e32 v42, v45, v24
	v_pk_mul_f32 v[24:25], v[14:15], s[56:57] op_sel_hi:[0,1] neg_lo:[1,0]
	v_pk_fma_f32 v[74:75], v[10:11], s[18:19], v[24:25] op_sel_hi:[0,1,1]
	v_lshlrev_b32_e32 v24, 16, v38
	v_add_f32_e32 v38, v49, v24
	v_pk_mul_f32 v[24:25], v[14:15], s[62:63] op_sel_hi:[0,1] neg_lo:[1,0]
	v_pk_fma_f32 v[72:73], v[10:11], s[92:93], v[24:25] op_sel_hi:[0,1,1]
	v_lshlrev_b32_e32 v25, 16, v39
	v_add_f32_e32 v32, v63, v25
	global_load_ushort v25, v[26:27], off offset:1024
	global_load_ushort v39, v[26:27], off offset:2048
	v_lshlrev_b32_e32 v24, 16, v40
	global_load_ushort v40, v[26:27], off offset:3072
	v_pk_mul_f32 v[30:31], v[14:15], s[58:59] op_sel_hi:[0,1] neg_lo:[1,0]
	v_pk_fma_f32 v[66:67], v[10:11], s[82:83], v[30:31] op_sel_hi:[0,1,1]
	v_pk_mul_f32 v[30:31], v[14:15], s[74:75] op_sel_hi:[0,1] neg_lo:[1,0]
	v_pk_fma_f32 v[76:77], v[10:11], s[28:29], v[30:31] op_sel_hi:[0,1,1]
	v_pk_mul_f32 v[30:31], v[14:15], s[30:31] op_sel_hi:[0,1] neg_lo:[1,0]
	v_pk_fma_f32 v[68:69], v[10:11], s[8:9], v[30:31] op_sel_hi:[0,1,1]
	v_pk_mul_f32 v[30:31], v[14:15], s[34:35] op_sel_hi:[0,1] neg_lo:[1,0]
	v_pk_fma_f32 v[70:71], v[10:11], s[4:5], v[30:31] op_sel_hi:[0,1,1]
	v_lshlrev_b32_e32 v30, 16, v98
	v_pk_mul_f32 v[34:35], v[14:15], s[36:37] op_sel_hi:[0,1] neg_lo:[1,0]
	v_add_f32_e32 v30, v90, v30
	v_pk_fma_f32 v[34:35], v[10:11], s[96:97], v[34:35] op_sel_hi:[0,1,1]
	v_pk_mul_f32 v[36:37], v[34:35], v[30:31] op_sel_hi:[1,0]
	v_pk_mul_f32 v[30:31], v[14:15], s[2:3] op_sel_hi:[0,1] neg_lo:[1,0]
	v_add_f32_e32 v26, v59, v13
	v_pk_fma_f32 v[30:31], v[10:11], s[0:1], v[30:31] op_sel_hi:[0,1,1]
	v_lshlrev_b32_e32 v13, 16, v15
	s_mov_b32 s4, s7
	s_mov_b32 s5, s9
	v_pk_mul_f32 v[34:35], v[14:15], s[6:7] op_sel_hi:[0,1] neg_lo:[1,0]
	v_pk_mul_f32 v[26:27], v[30:31], v[26:27] op_sel_hi:[1,0]
	v_add_f32_e32 v30, v57, v13
	v_pk_fma_f32 v[34:35], v[10:11], s[4:5], v[34:35] op_sel_hi:[0,1,1]
	v_pk_mul_f32 v[98:99], v[34:35], v[30:31] op_sel_hi:[1,0]
	s_waitcnt vmcnt(4)
	v_lshlrev_b32_e32 v13, 16, v21
	s_mov_b32 s8, s81
	s_mov_b32 s9, s93
	v_pk_mul_f32 v[34:35], v[14:15], s[10:11] op_sel_hi:[0,1] neg_lo:[1,0]
	v_add_f32_e32 v30, v55, v13
	v_pk_fma_f32 v[34:35], v[10:11], s[8:9], v[34:35] op_sel_hi:[0,1,1]
	v_pk_mul_f32 v[100:101], v[34:35], v[30:31] op_sel_hi:[1,0]
	s_waitcnt vmcnt(3)
	v_lshlrev_b32_e32 v13, 16, v23
	v_pk_mul_f32 v[34:35], v[14:15], s[16:17] op_sel_hi:[0,1] neg_lo:[1,0]
	v_add_f32_e32 v30, v97, v13
	v_pk_fma_f32 v[34:35], v[10:11], s[12:13], v[34:35] op_sel_hi:[0,1,1]
	v_pk_mul_f32 v[102:103], v[34:35], v[30:31] op_sel_hi:[1,0]
	v_lshlrev_b32_e32 v13, 16, v53
	s_mov_b32 s18, s21
	s_mov_b32 s19, s89
	v_pk_mul_f32 v[34:35], v[14:15], s[20:21] op_sel_hi:[0,1] neg_lo:[1,0]
	v_add_f32_e32 v30, v96, v13
	v_pk_fma_f32 v[34:35], v[10:11], s[18:19], v[34:35] op_sel_hi:[0,1,1]
	s_mov_b32 s24, s25
	s_mov_b32 s25, s83
	v_pk_mul_f32 v[96:97], v[34:35], v[30:31] op_sel_hi:[1,0]
	v_lshlrev_b32_e32 v13, 16, v51
	v_pk_mul_f32 v[34:35], v[14:15], s[24:25] op_sel_hi:[0,1] neg_lo:[1,0]
	v_add_f32_e32 v30, v94, v13
	v_pk_fma_f32 v[34:35], v[10:11], s[22:23], v[34:35] op_sel_hi:[0,1,1]
	s_mov_b32 s28, s87
	v_pk_mul_f32 v[104:105], v[34:35], v[30:31] op_sel_hi:[1,0]
	v_lshlrev_b32_e32 v13, 16, v91
	v_pk_mul_f32 v[34:35], v[14:15], s[28:29] op_sel_hi:[0,1] neg_lo:[1,0]
	v_add_f32_e32 v30, v93, v13
	v_pk_fma_f32 v[34:35], v[10:11], s[26:27], v[34:35] op_sel_hi:[0,1,1]
	v_pk_mul_f32 v[90:91], v[34:35], v[30:31] op_sel_hi:[1,0]
	v_lshlrev_b32_e32 v13, 16, v33
	v_pk_mul_f32 v[34:35], v[14:15], s[84:85] op_sel_hi:[0,0] neg_lo:[1,0]
	v_add_f32_e32 v30, v92, v13
	v_pk_fma_f32 v[34:35], v[10:11], s[38:39], v[34:35] op_sel_hi:[0,0,1] neg_lo:[0,0,1] neg_hi:[0,0,1]
	v_pk_mul_f32 v[92:93], v[34:35], v[30:31] op_sel_hi:[1,0]
	v_pk_mul_f32 v[34:35], v[14:15], s[26:27] op_sel_hi:[0,1] neg_lo:[1,0]
	v_pk_fma_f32 v[34:35], v[10:11], s[28:29], v[34:35] op_sel_hi:[0,1,1]
	v_add_f32_e32 v24, v61, v24
	s_waitcnt vmcnt(2)
	v_lshlrev_b32_e32 v13, 16, v25
	v_add_f32_e32 v30, v95, v13
	v_pk_mul_f32 v[94:95], v[34:35], v[30:31] op_sel_hi:[1,0]
	s_waitcnt vmcnt(1)
	v_lshlrev_b32_e32 v13, 16, v39
	v_pk_mul_f32 v[34:35], v[14:15], s[22:23] op_sel_hi:[0,1] neg_lo:[1,0]
	v_add_f32_e32 v30, v106, v13
	v_pk_fma_f32 v[34:35], v[10:11], s[24:25], v[34:35] op_sel_hi:[0,1,1]
	v_pk_mul_f32 v[106:107], v[34:35], v[30:31] op_sel_hi:[1,0]
	s_waitcnt vmcnt(0)
	v_lshlrev_b32_e32 v13, 16, v40
	v_pk_mul_f32 v[34:35], v[14:15], s[18:19] op_sel_hi:[0,1] neg_lo:[1,0]
	v_add_f32_e32 v30, v108, v13
	v_pk_fma_f32 v[34:35], v[10:11], s[20:21], v[34:35] op_sel_hi:[0,1,1]
	v_pk_mul_f32 v[108:109], v[34:35], v[30:31] op_sel_hi:[1,0]
	v_lshlrev_b32_e32 v13, 16, v110
	v_pk_mul_f32 v[34:35], v[14:15], s[12:13] op_sel_hi:[0,1] neg_lo:[1,0]
	v_add_f32_e32 v30, v111, v13
	v_pk_fma_f32 v[34:35], v[10:11], s[16:17], v[34:35] op_sel_hi:[0,1,1]
	v_pk_mul_f32 v[110:111], v[34:35], v[30:31] op_sel_hi:[1,0]
	v_lshlrev_b32_e32 v13, 16, v112
	v_pk_mul_f32 v[34:35], v[14:15], s[8:9] op_sel_hi:[0,1] neg_lo:[1,0]
	v_add_f32_e32 v30, v113, v13
	v_pk_fma_f32 v[34:35], v[10:11], s[10:11], v[34:35] op_sel_hi:[0,1,1]
	v_pk_mul_f32 v[112:113], v[34:35], v[30:31] op_sel_hi:[1,0]
	v_lshlrev_b32_e32 v13, 16, v114
	v_pk_mul_f32 v[34:35], v[14:15], s[4:5] op_sel_hi:[0,1] neg_lo:[1,0]
	v_add_f32_e32 v30, v115, v13
	v_pk_fma_f32 v[34:35], v[10:11], s[6:7], v[34:35] op_sel_hi:[0,1,1]
	v_lshlrev_b32_e32 v13, 16, v116
	v_pk_mul_f32 v[14:15], v[14:15], s[0:1] op_sel_hi:[0,1] neg_lo:[1,0]
	v_pk_mul_f32 v[114:115], v[34:35], v[30:31] op_sel_hi:[1,0]
	v_add_f32_e32 v30, v17, v13
	v_pk_fma_f32 v[14:15], v[10:11], s[2:3], v[14:15] op_sel_hi:[0,1,1]
	v_pk_mul_f32 v[116:117], v[14:15], v[30:31] op_sel_hi:[1,0]
	v_mov_b32_e32 v13, v173
	v_mov_b32_e32 v14, v178
	v_mov_b32_e32 v15, v179
	v_mov_b32_e32 v10, v1
	v_mov_b32_e32 v30, v165
	v_mov_b32_e32 v10, v167
	v_mov_b32_e32 v34, v169
	v_mov_b32_e32 v17, v171
	s_nop 0
	v_pk_fma_f32 v[126:127], v[18:19], v[16:17], v[36:37] op_sel_hi:[1,0,1]
	v_pk_fma_f32 v[36:37], v[18:19], v[16:17], v[36:37] op_sel_hi:[1,0,1] neg_lo:[0,0,1] neg_hi:[0,0,1]
	v_pk_fma_f32 v[18:19], v[28:29], v[20:21], v[26:27] op_sel_hi:[1,0,1] neg_lo:[0,0,1] neg_hi:[0,0,1]
	v_pk_fma_f32 v[16:17], v[28:29], v[20:21], v[26:27] op_sel_hi:[1,0,1]
	v_xor_b32_e32 v20, 0x80000000, v19
	v_mov_b32_e32 v21, v18
	v_pk_mul_f32 v[20:21], v[20:21], v[124:125] op_sel_hi:[1,0] neg_lo:[0,1] neg_hi:[0,1]
	s_nop 0
	v_pk_fma_f32 v[40:41], v[18:19], v[118:119], v[20:21] op_sel_hi:[1,0,1]
	v_pk_fma_f32 v[20:21], v[46:47], v[22:23], v[98:99] op_sel_hi:[1,0,1] neg_lo:[0,0,1] neg_hi:[0,0,1]
	v_pk_fma_f32 v[18:19], v[46:47], v[22:23], v[98:99] op_sel_hi:[1,0,1]
	v_xor_b32_e32 v22, 0x80000000, v21
	v_mov_b32_e32 v23, v20
	v_pk_mul_f32 v[22:23], v[22:23], v[34:35] op_sel_hi:[1,0] neg_lo:[0,1] neg_hi:[0,1]
	s_nop 0
	v_pk_fma_f32 v[46:47], v[20:21], v[30:31], v[22:23] op_sel_hi:[1,0,1]
	v_pk_fma_f32 v[22:23], v[88:89], v[50:51], v[100:101] op_sel_hi:[1,0,1] neg_lo:[0,0,1] neg_hi:[0,0,1]
	v_pk_fma_f32 v[20:21], v[88:89], v[50:51], v[100:101] op_sel_hi:[1,0,1]
	v_xor_b32_e32 v26, 0x80000000, v23
	v_mov_b32_e32 v27, v22
	v_pk_mul_f32 v[26:27], v[26:27], v[122:123] op_sel_hi:[1,0] neg_lo:[0,1] neg_hi:[0,1]
	s_nop 0
	v_pk_fma_f32 v[50:51], v[22:23], v[120:121], v[26:27] op_sel_hi:[1,0,1]
	v_pk_fma_f32 v[26:27], v[84:85], v[52:53], v[102:103] op_sel_hi:[1,0,1] neg_lo:[0,0,1] neg_hi:[0,0,1]
	v_pk_fma_f32 v[22:23], v[84:85], v[52:53], v[102:103] op_sel_hi:[1,0,1]
	v_xor_b32_e32 v28, 0x80000000, v27
	v_mov_b32_e32 v29, v26
	v_pk_mul_f32 v[28:29], v[28:29], v[10:11] op_sel_hi:[1,0] neg_lo:[0,1] neg_hi:[0,1]
	s_nop 0
	v_pk_fma_f32 v[52:53], v[26:27], v[10:11], v[28:29] op_sel_hi:[1,0,1]
	v_pk_fma_f32 v[28:29], v[64:65], v[44:45], v[96:97] op_sel_hi:[1,0,1] neg_lo:[0,0,1] neg_hi:[0,0,1]
	v_pk_fma_f32 v[26:27], v[64:65], v[44:45], v[96:97] op_sel_hi:[1,0,1]
	v_pk_mul_f32 v[44:45], v[28:29], v[122:123] op_sel_hi:[1,0]
	v_xor_b32_e32 v64, 0x80000000, v29
	v_mov_b32_e32 v65, v28
	v_pk_fma_f32 v[64:65], v[64:65], v[120:121], v[44:45] op_sel_hi:[1,0,1] neg_lo:[0,1,0] neg_hi:[0,1,0]
	v_pk_fma_f32 v[44:45], v[66:67], v[48:49], v[104:105] op_sel_hi:[1,0,1] neg_lo:[0,0,1] neg_hi:[0,0,1]
	v_pk_fma_f32 v[28:29], v[66:67], v[48:49], v[104:105] op_sel_hi:[1,0,1]
	v_pk_mul_f32 v[48:49], v[44:45], v[34:35] op_sel_hi:[1,0]
	v_xor_b32_e32 v66, 0x80000000, v45
	v_mov_b32_e32 v67, v44
	v_pk_fma_f32 v[66:67], v[66:67], v[30:31], v[48:49] op_sel_hi:[1,0,1] neg_lo:[0,1,0] neg_hi:[0,1,0]
	v_pk_fma_f32 v[48:49], v[76:77], v[54:55], v[90:91] op_sel_hi:[1,0,1] neg_lo:[0,0,1] neg_hi:[0,0,1]
	v_pk_fma_f32 v[44:45], v[76:77], v[54:55], v[90:91] op_sel_hi:[1,0,1]
	v_pk_mul_f32 v[54:55], v[48:49], v[124:125] op_sel_hi:[1,0]
	v_xor_b32_e32 v76, 0x80000000, v49
	v_mov_b32_e32 v77, v48
	v_pk_fma_f32 v[48:49], v[78:79], v[56:57], v[92:93] op_sel_hi:[1,0,1]
	v_pk_fma_f32 v[56:57], v[78:79], v[56:57], v[92:93] op_sel_hi:[1,0,1] neg_lo:[0,0,1] neg_hi:[0,0,1]
	v_pk_fma_f32 v[54:55], v[76:77], v[118:119], v[54:55] op_sel_hi:[1,0,1] neg_lo:[0,1,0] neg_hi:[0,1,0]
	v_xor_b32_e32 v77, 0x80000000, v56
	v_mov_b32_e32 v76, v57
	v_pk_fma_f32 v[56:57], v[86:87], v[60:61], v[94:95] op_sel_hi:[1,0,1]
	v_pk_fma_f32 v[60:61], v[86:87], v[60:61], v[94:95] op_sel_hi:[1,0,1] neg_lo:[0,0,1] neg_hi:[0,0,1]
	s_nop 0
	v_pk_mul_f32 v[78:79], v[60:61], v[124:125] op_sel_hi:[1,0] neg_lo:[0,1] neg_hi:[0,1]
	v_xor_b32_e32 v84, 0x80000000, v61
	v_mov_b32_e32 v85, v60
	v_pk_fma_f32 v[60:61], v[84:85], v[118:119], v[78:79] op_sel_hi:[1,0,1] neg_lo:[0,1,0] neg_hi:[0,1,0]
	v_pk_fma_f32 v[78:79], v[82:83], v[62:63], v[106:107] op_sel_hi:[1,0,1]
	v_pk_fma_f32 v[62:63], v[82:83], v[62:63], v[106:107] op_sel_hi:[1,0,1] neg_lo:[0,0,1] neg_hi:[0,0,1]
	s_nop 0
	v_pk_mul_f32 v[82:83], v[62:63], v[34:35] op_sel_hi:[1,0] neg_lo:[0,1] neg_hi:[0,1]
	v_xor_b32_e32 v84, 0x80000000, v63
	v_mov_b32_e32 v85, v62
	v_pk_fma_f32 v[62:63], v[84:85], v[30:31], v[82:83] op_sel_hi:[1,0,1] neg_lo:[0,1,0] neg_hi:[0,1,0]
	v_pk_fma_f32 v[82:83], v[80:81], v[58:59], v[108:109] op_sel_hi:[1,0,1]
	v_pk_fma_f32 v[58:59], v[80:81], v[58:59], v[108:109] op_sel_hi:[1,0,1] neg_lo:[0,0,1] neg_hi:[0,0,1]
	s_nop 0
	v_pk_mul_f32 v[80:81], v[58:59], v[122:123] op_sel_hi:[1,0] neg_lo:[0,1] neg_hi:[0,1]
	v_xor_b32_e32 v84, 0x80000000, v59
	v_mov_b32_e32 v85, v58
	v_pk_fma_f32 v[58:59], v[84:85], v[120:121], v[80:81] op_sel_hi:[1,0,1] neg_lo:[0,1,0] neg_hi:[0,1,0]
	v_pk_add_f32 v[84:85], v[16:17], v[56:57]
	v_pk_add_f32 v[16:17], v[16:17], v[56:57] neg_lo:[0,1] neg_hi:[0,1]
	v_pk_fma_f32 v[80:81], v[74:75], v[42:43], v[110:111] op_sel_hi:[1,0,1]
	v_xor_b32_e32 v56, 0x80000000, v17
	v_mov_b32_e32 v57, v16
	v_pk_mul_f32 v[56:57], v[56:57], v[34:35] op_sel_hi:[1,0] neg_lo:[0,1] neg_hi:[0,1]
	v_pk_fma_f32 v[42:43], v[74:75], v[42:43], v[110:111] op_sel_hi:[1,0,1] neg_lo:[0,0,1] neg_hi:[0,0,1]
	v_pk_fma_f32 v[56:57], v[16:17], v[30:31], v[56:57] op_sel_hi:[1,0,1]
	v_pk_add_f32 v[16:17], v[18:19], v[78:79]
	v_pk_add_f32 v[18:19], v[18:19], v[78:79] neg_lo:[0,1] neg_hi:[0,1]
	v_xor_b32_e32 v74, 0x80000000, v43
	v_mov_b32_e32 v75, v42
	v_xor_b32_e32 v78, 0x80000000, v19
	v_mov_b32_e32 v79, v18
	v_pk_mul_f32 v[74:75], v[74:75], v[10:11] op_sel_hi:[1,0] neg_lo:[0,1] neg_hi:[0,1]
	v_pk_mul_f32 v[78:79], v[78:79], v[10:11] op_sel_hi:[1,0] neg_lo:[0,1] neg_hi:[0,1]
	v_pk_fma_f32 v[74:75], v[42:43], v[10:11], v[74:75] op_sel_hi:[1,0,1] neg_lo:[0,1,0] neg_hi:[0,1,0]
	v_pk_fma_f32 v[42:43], v[72:73], v[38:39], v[112:113] op_sel_hi:[1,0,1]
	v_pk_fma_f32 v[38:39], v[72:73], v[38:39], v[112:113] op_sel_hi:[1,0,1] neg_lo:[0,0,1] neg_hi:[0,0,1]
	v_pk_fma_f32 v[18:19], v[18:19], v[10:11], v[78:79] op_sel_hi:[1,0,1]
	v_pk_add_f32 v[78:79], v[20:21], v[82:83]
	v_pk_add_f32 v[20:21], v[20:21], v[82:83] neg_lo:[0,1] neg_hi:[0,1]
	v_xor_b32_e32 v72, 0x80000000, v39
	v_mov_b32_e32 v73, v38
	v_pk_mul_f32 v[82:83], v[20:21], v[34:35] op_sel_hi:[1,0]
	v_xor_b32_e32 v86, 0x80000000, v21
	v_mov_b32_e32 v87, v20
	v_pk_add_f32 v[20:21], v[22:23], v[80:81]
	v_pk_add_f32 v[22:23], v[22:23], v[80:81] neg_lo:[0,1] neg_hi:[0,1]
	v_pk_mul_f32 v[72:73], v[72:73], v[122:123] op_sel_hi:[1,0] neg_lo:[0,1] neg_hi:[0,1]
	v_xor_b32_e32 v81, 0x80000000, v22
	v_mov_b32_e32 v80, v23
	v_pk_add_f32 v[22:23], v[26:27], v[42:43]
	v_pk_add_f32 v[26:27], v[26:27], v[42:43] neg_lo:[0,1] neg_hi:[0,1]
	v_pk_fma_f32 v[72:73], v[38:39], v[120:121], v[72:73] op_sel_hi:[1,0,1] neg_lo:[0,1,0] neg_hi:[0,1,0]
	v_pk_fma_f32 v[38:39], v[68:69], v[24:25], v[114:115] op_sel_hi:[1,0,1]
	v_pk_fma_f32 v[24:25], v[68:69], v[24:25], v[114:115] op_sel_hi:[1,0,1] neg_lo:[0,0,1] neg_hi:[0,0,1]
	v_pk_fma_f32 v[82:83], v[86:87], v[30:31], v[82:83] op_sel_hi:[1,0,1] neg_lo:[0,1,0] neg_hi:[0,1,0]
	v_pk_mul_f32 v[42:43], v[26:27], v[34:35] op_sel_hi:[1,0] neg_lo:[0,1] neg_hi:[0,1]
	v_xor_b32_e32 v86, 0x80000000, v27
	v_mov_b32_e32 v87, v26
	v_xor_b32_e32 v68, 0x80000000, v25
	v_mov_b32_e32 v69, v24
	v_pk_fma_f32 v[26:27], v[30:31], v[86:87], v[42:43] op_sel_hi:[0,1,1] neg_lo:[1,0,0] neg_hi:[1,0,0]
	v_pk_add_f32 v[42:43], v[28:29], v[38:39]
	v_pk_add_f32 v[28:29], v[28:29], v[38:39] neg_lo:[0,1] neg_hi:[0,1]
	v_pk_mul_f32 v[68:69], v[68:69], v[34:35] op_sel_hi:[1,0] neg_lo:[0,1] neg_hi:[0,1]
	v_xor_b32_e32 v38, 0x80000000, v29
	v_mov_b32_e32 v39, v28
	v_pk_fma_f32 v[68:69], v[24:25], v[30:31], v[68:69] op_sel_hi:[1,0,1] neg_lo:[0,1,0] neg_hi:[0,1,0]
	v_pk_fma_f32 v[24:25], v[70:71], v[32:33], v[116:117] op_sel_hi:[1,0,1]
	v_pk_fma_f32 v[32:33], v[70:71], v[32:33], v[116:117] op_sel_hi:[1,0,1] neg_lo:[0,0,1] neg_hi:[0,0,1]
	v_pk_mul_f32 v[38:39], v[10:11], v[38:39] op_sel_hi:[0,1] neg_lo:[1,0] neg_hi:[1,0]
	v_xor_b32_e32 v70, 0x80000000, v33
	v_mov_b32_e32 v71, v32
	v_pk_fma_f32 v[86:87], v[28:29], v[10:11], v[38:39] op_sel_hi:[1,0,1] neg_lo:[0,1,0] neg_hi:[0,1,0]
	v_pk_add_f32 v[28:29], v[44:45], v[24:25]
	v_pk_add_f32 v[24:25], v[44:45], v[24:25] neg_lo:[0,1] neg_hi:[0,1]
	v_pk_mul_f32 v[70:71], v[70:71], v[124:125] op_sel_hi:[1,0] neg_lo:[0,1] neg_hi:[0,1]
	v_xor_b32_e32 v38, 0x80000000, v25
	v_mov_b32_e32 v39, v24
	v_pk_fma_f32 v[70:71], v[118:119], v[32:33], v[70:71] op_sel_hi:[0,1,1] neg_lo:[1,0,0] neg_hi:[1,0,0]
	v_pk_add_f32 v[32:33], v[126:127], v[48:49]
	v_pk_mul_f32 v[38:39], v[34:35], v[38:39] op_sel_hi:[0,1] neg_lo:[1,0] neg_hi:[1,0]
	v_pk_fma_f32 v[88:89], v[30:31], v[24:25], v[38:39] op_sel_hi:[0,1,1] neg_lo:[1,0,0] neg_hi:[1,0,0]
	v_pk_add_f32 v[24:25], v[32:33], v[20:21]
	v_pk_add_f32 v[32:33], v[32:33], v[20:21] neg_lo:[0,1] neg_hi:[0,1]
	v_pk_add_f32 v[20:21], v[84:85], v[22:23]
	v_pk_add_f32 v[22:23], v[84:85], v[22:23] neg_lo:[0,1] neg_hi:[0,1]
	v_pk_add_f32 v[48:49], v[126:127], v[48:49] neg_lo:[0,1] neg_hi:[0,1]
	v_xor_b32_e32 v38, 0x80000000, v23
	v_mov_b32_e32 v39, v22
	v_pk_mul_f32 v[38:39], v[10:11], v[38:39] op_sel_hi:[0,1] neg_lo:[1,0] neg_hi:[1,0]
	v_pk_fma_f32 v[22:23], v[22:23], v[10:11], v[38:39] op_sel_hi:[1,0,1]
	v_pk_add_f32 v[38:39], v[16:17], v[42:43]
	v_pk_add_f32 v[16:17], v[16:17], v[42:43] neg_lo:[0,1] neg_hi:[0,1]
	s_nop 0
	v_xor_b32_e32 v43, 0x80000000, v16
	v_mov_b32_e32 v42, v17
	v_pk_add_f32 v[16:17], v[78:79], v[28:29]
	v_pk_add_f32 v[28:29], v[78:79], v[28:29] neg_lo:[0,1] neg_hi:[0,1]
	s_nop 0
	v_xor_b32_e32 v44, 0x80000000, v29
	v_mov_b32_e32 v45, v28
	v_pk_mul_f32 v[44:45], v[10:11], v[44:45] op_sel_hi:[0,1] neg_lo:[1,0] neg_hi:[1,0]
	v_pk_fma_f32 v[78:79], v[10:11], v[28:29], v[44:45] op_sel_hi:[0,1,1] neg_lo:[1,0,0] neg_hi:[1,0,0]
	v_pk_add_f32 v[28:29], v[24:25], v[38:39]
	v_pk_add_f32 v[24:25], v[24:25], v[38:39] neg_lo:[0,1] neg_hi:[0,1]
	v_pk_add_f32 v[38:39], v[20:21], v[16:17]
	v_pk_add_f32 v[16:17], v[20:21], v[16:17] neg_lo:[0,1] neg_hi:[0,1]
	v_pk_add_f32 v[84:85], v[28:29], v[38:39]
	v_xor_b32_e32 v21, 0x80000000, v16
	v_mov_b32_e32 v20, v17
	v_pk_add_f32 v[44:45], v[24:25], v[20:21]
	v_pk_add_f32 v[20:21], v[24:25], v[20:21] neg_lo:[0,1] neg_hi:[0,1]
	v_pk_add_f32 v[24:25], v[22:23], v[78:79]
	v_pk_add_f32 v[22:23], v[22:23], v[78:79] neg_lo:[0,1] neg_hi:[0,1]
	v_pk_add_f32 v[16:17], v[32:33], v[42:43]
	v_pk_add_f32 v[32:33], v[32:33], v[42:43] neg_lo:[0,1] neg_hi:[0,1]
	v_xor_b32_e32 v43, 0x80000000, v22
	v_mov_b32_e32 v42, v23
	v_pk_add_f32 v[28:29], v[28:29], v[38:39] neg_lo:[0,1] neg_hi:[0,1]
	v_pk_add_f32 v[78:79], v[16:17], v[24:25]
	v_pk_add_f32 v[24:25], v[16:17], v[24:25] neg_lo:[0,1] neg_hi:[0,1]
	v_pk_add_f32 v[38:39], v[32:33], v[42:43]
	v_pk_add_f32 v[16:17], v[32:33], v[42:43] neg_lo:[0,1] neg_hi:[0,1]
	v_pk_add_f32 v[32:33], v[56:57], v[26:27]
	v_pk_add_f32 v[26:27], v[56:57], v[26:27] neg_lo:[0,1] neg_hi:[0,1]
	v_pk_add_f32 v[22:23], v[48:49], v[80:81]
	v_pk_add_f32 v[42:43], v[48:49], v[80:81] neg_lo:[0,1] neg_hi:[0,1]
	v_xor_b32_e32 v48, 0x80000000, v27
	v_mov_b32_e32 v49, v26
	v_pk_mul_f32 v[48:49], v[10:11], v[48:49] op_sel_hi:[0,1] neg_lo:[1,0] neg_hi:[1,0]
	v_pk_fma_f32 v[26:27], v[10:11], v[26:27], v[48:49] op_sel_hi:[0,1,1]
	v_pk_add_f32 v[48:49], v[18:19], v[86:87]
	v_pk_add_f32 v[18:19], v[18:19], v[86:87] neg_lo:[0,1] neg_hi:[0,1]
	v_pk_add_f32 v[80:81], v[82:83], v[88:89] neg_lo:[0,1] neg_hi:[0,1]
	v_xor_b32_e32 v57, 0x80000000, v18
	v_mov_b32_e32 v56, v19
	v_pk_add_f32 v[18:19], v[82:83], v[88:89]
	v_xor_b32_e32 v82, 0x80000000, v81
	v_mov_b32_e32 v83, v80
	v_pk_mul_f32 v[82:83], v[10:11], v[82:83] op_sel_hi:[0,1] neg_lo:[1,0] neg_hi:[1,0]
	v_pk_fma_f32 v[80:81], v[10:11], v[80:81], v[82:83] op_sel_hi:[0,1,1] neg_lo:[1,0,0] neg_hi:[1,0,0]
	v_pk_add_f32 v[82:83], v[22:23], v[48:49]
	v_pk_add_f32 v[22:23], v[22:23], v[48:49] neg_lo:[0,1] neg_hi:[0,1]
	v_pk_add_f32 v[48:49], v[32:33], v[18:19]
	v_pk_add_f32 v[18:19], v[32:33], v[18:19] neg_lo:[0,1] neg_hi:[0,1]
	v_pk_add_f32 v[88:89], v[82:83], v[48:49]
	v_xor_b32_e32 v87, 0x80000000, v18
	v_mov_b32_e32 v86, v19
	v_pk_add_f32 v[18:19], v[42:43], v[56:57]
	v_pk_add_f32 v[56:57], v[42:43], v[56:57] neg_lo:[0,1] neg_hi:[0,1]
	v_pk_add_f32 v[42:43], v[26:27], v[80:81]
	v_pk_add_f32 v[26:27], v[26:27], v[80:81] neg_lo:[0,1] neg_hi:[0,1]
	v_pk_add_f32 v[32:33], v[82:83], v[48:49] neg_lo:[0,1] neg_hi:[0,1]
	v_xor_b32_e32 v81, 0x80000000, v26
	v_mov_b32_e32 v80, v27
	v_pk_add_f32 v[82:83], v[18:19], v[42:43]
	v_pk_add_f32 v[26:27], v[18:19], v[42:43] neg_lo:[0,1] neg_hi:[0,1]
	v_pk_add_f32 v[42:43], v[56:57], v[80:81]
	v_pk_add_f32 v[18:19], v[56:57], v[80:81] neg_lo:[0,1] neg_hi:[0,1]
	v_pk_add_f32 v[56:57], v[36:37], v[76:77]
	v_pk_add_f32 v[76:77], v[36:37], v[76:77] neg_lo:[0,1] neg_hi:[0,1]
	v_pk_add_f32 v[36:37], v[40:41], v[60:61]
	v_pk_add_f32 v[40:41], v[40:41], v[60:61] neg_lo:[0,1] neg_hi:[0,1]
	v_pk_add_f32 v[48:49], v[22:23], v[86:87]
	v_xor_b32_e32 v60, 0x80000000, v41
	v_mov_b32_e32 v61, v40
	v_pk_mul_f32 v[60:61], v[34:35], v[60:61] op_sel_hi:[0,1] neg_lo:[1,0] neg_hi:[1,0]
	v_pk_fma_f32 v[40:41], v[30:31], v[40:41], v[60:61] op_sel_hi:[0,1,1]
	v_pk_add_f32 v[60:61], v[46:47], v[62:63]
	v_pk_add_f32 v[46:47], v[46:47], v[62:63] neg_lo:[0,1] neg_hi:[0,1]
	v_pk_add_f32 v[22:23], v[22:23], v[86:87] neg_lo:[0,1] neg_hi:[0,1]
	v_xor_b32_e32 v62, 0x80000000, v47
	v_mov_b32_e32 v63, v46
	v_pk_mul_f32 v[62:63], v[10:11], v[62:63] op_sel_hi:[0,1] neg_lo:[1,0] neg_hi:[1,0]
	v_pk_fma_f32 v[62:63], v[10:11], v[46:47], v[62:63] op_sel_hi:[0,1,1]
	v_pk_add_f32 v[46:47], v[50:51], v[58:59]
	v_pk_add_f32 v[50:51], v[50:51], v[58:59] neg_lo:[0,1] neg_hi:[0,1]
	s_nop 0
	v_xor_b32_e32 v58, 0x80000000, v51
	v_mov_b32_e32 v59, v50
	v_pk_mul_f32 v[58:59], v[30:31], v[58:59] op_sel_hi:[0,1] neg_lo:[1,0] neg_hi:[1,0]
	v_pk_fma_f32 v[50:51], v[34:35], v[50:51], v[58:59] op_sel_hi:[0,1,1]
	v_pk_add_f32 v[58:59], v[52:53], v[74:75]
	v_pk_add_f32 v[52:53], v[52:53], v[74:75] neg_lo:[0,1] neg_hi:[0,1]
	s_nop 0
	v_xor_b32_e32 v75, 0x80000000, v52
	v_mov_b32_e32 v74, v53
	v_pk_add_f32 v[52:53], v[64:65], v[72:73]
	v_pk_add_f32 v[64:65], v[64:65], v[72:73] neg_lo:[0,1] neg_hi:[0,1]
	s_nop 0
	v_xor_b32_e32 v72, 0x80000000, v65
	v_mov_b32_e32 v73, v64
	v_pk_mul_f32 v[72:73], v[30:31], v[72:73] op_sel_hi:[0,1] neg_lo:[1,0] neg_hi:[1,0]
	v_pk_fma_f32 v[64:65], v[34:35], v[64:65], v[72:73] op_sel_hi:[0,1,1] neg_lo:[1,0,0] neg_hi:[1,0,0]
	v_pk_add_f32 v[72:73], v[66:67], v[68:69]
	v_pk_add_f32 v[66:67], v[66:67], v[68:69] neg_lo:[0,1] neg_hi:[0,1]
	s_nop 0
	v_xor_b32_e32 v68, 0x80000000, v67
	v_mov_b32_e32 v69, v66
	v_pk_mul_f32 v[68:69], v[10:11], v[68:69] op_sel_hi:[0,1] neg_lo:[1,0] neg_hi:[1,0]
	v_pk_fma_f32 v[66:67], v[10:11], v[66:67], v[68:69] op_sel_hi:[0,1,1] neg_lo:[1,0,0] neg_hi:[1,0,0]
	v_pk_add_f32 v[68:69], v[54:55], v[70:71]
	v_pk_add_f32 v[54:55], v[54:55], v[70:71] neg_lo:[0,1] neg_hi:[0,1]
	s_nop 0
	v_xor_b32_e32 v70, 0x80000000, v55
	v_mov_b32_e32 v71, v54
	v_pk_mul_f32 v[34:35], v[34:35], v[70:71] op_sel_hi:[0,1] neg_lo:[1,0] neg_hi:[1,0]
	v_pk_fma_f32 v[34:35], v[30:31], v[54:55], v[34:35] op_sel_hi:[0,1,1] neg_lo:[1,0,0] neg_hi:[1,0,0]
	v_pk_add_f32 v[30:31], v[56:57], v[58:59]
	v_pk_add_f32 v[54:55], v[56:57], v[58:59] neg_lo:[0,1] neg_hi:[0,1]
	v_pk_add_f32 v[56:57], v[52:53], v[36:37]
	v_pk_add_f32 v[36:37], v[36:37], v[52:53] neg_lo:[0,1] neg_hi:[0,1]
	s_nop 0
	v_xor_b32_e32 v52, 0x80000000, v37
	v_mov_b32_e32 v53, v36
	v_pk_mul_f32 v[52:53], v[10:11], v[52:53] op_sel_hi:[0,1] neg_lo:[1,0] neg_hi:[1,0]
	v_pk_fma_f32 v[58:59], v[10:11], v[36:37], v[52:53] op_sel_hi:[0,1,1]
	v_pk_add_f32 v[52:53], v[60:61], v[72:73] neg_lo:[0,1] neg_hi:[0,1]
	v_pk_add_f32 v[36:37], v[60:61], v[72:73]
	v_xor_b32_e32 v61, 0x80000000, v52
	v_mov_b32_e32 v60, v53
	v_pk_add_f32 v[52:53], v[46:47], v[68:69]
	v_pk_add_f32 v[46:47], v[46:47], v[68:69] neg_lo:[0,1] neg_hi:[0,1]
	v_pk_add_f32 v[72:73], v[64:65], v[40:41]
	v_xor_b32_e32 v68, 0x80000000, v47
	v_mov_b32_e32 v69, v46
	v_pk_add_f32 v[40:41], v[40:41], v[64:65] neg_lo:[0,1] neg_hi:[0,1]
	v_pk_mul_f32 v[68:69], v[10:11], v[68:69] op_sel_hi:[0,1] neg_lo:[1,0] neg_hi:[1,0]
	v_xor_b32_e32 v64, 0x80000000, v41
	v_mov_b32_e32 v65, v40
	v_pk_fma_f32 v[46:47], v[10:11], v[46:47], v[68:69] op_sel_hi:[0,1,1] neg_lo:[1,0,0] neg_hi:[1,0,0]
	v_pk_add_f32 v[68:69], v[30:31], v[36:37]
	v_pk_add_f32 v[30:31], v[30:31], v[36:37] neg_lo:[0,1] neg_hi:[0,1]
	v_pk_add_f32 v[36:37], v[56:57], v[52:53]
	v_pk_add_f32 v[52:53], v[56:57], v[52:53] neg_lo:[0,1] neg_hi:[0,1]
	v_pk_mul_f32 v[64:65], v[10:11], v[64:65] op_sel_hi:[0,1] neg_lo:[1,0] neg_hi:[1,0]
	v_xor_b32_e32 v57, 0x80000000, v52
	v_mov_b32_e32 v56, v53
	v_pk_fma_f32 v[64:65], v[10:11], v[40:41], v[64:65] op_sel_hi:[0,1,1]
	v_pk_add_f32 v[40:41], v[62:63], v[66:67]
	v_pk_add_f32 v[62:63], v[62:63], v[66:67] neg_lo:[0,1] neg_hi:[0,1]
	v_pk_add_f32 v[70:71], v[68:69], v[36:37]
	v_pk_add_f32 v[52:53], v[68:69], v[36:37] neg_lo:[0,1] neg_hi:[0,1]
	v_pk_add_f32 v[68:69], v[30:31], v[56:57]
	v_pk_add_f32 v[36:37], v[30:31], v[56:57] neg_lo:[0,1] neg_hi:[0,1]
	v_pk_add_f32 v[56:57], v[58:59], v[46:47]
	v_pk_add_f32 v[46:47], v[58:59], v[46:47] neg_lo:[0,1] neg_hi:[0,1]
	v_xor_b32_e32 v67, 0x80000000, v62
	v_mov_b32_e32 v66, v63
	v_pk_add_f32 v[62:63], v[50:51], v[34:35]
	v_pk_add_f32 v[34:35], v[50:51], v[34:35] neg_lo:[0,1] neg_hi:[0,1]
	v_pk_add_f32 v[30:31], v[54:55], v[60:61]
	v_pk_add_f32 v[54:55], v[54:55], v[60:61] neg_lo:[0,1] neg_hi:[0,1]
	v_xor_b32_e32 v59, 0x80000000, v46
	v_mov_b32_e32 v58, v47
	v_xor_b32_e32 v50, 0x80000000, v35
	v_mov_b32_e32 v51, v34
	v_pk_add_f32 v[60:61], v[30:31], v[56:57]
	v_pk_add_f32 v[46:47], v[30:31], v[56:57] neg_lo:[0,1] neg_hi:[0,1]
	v_pk_add_f32 v[56:57], v[54:55], v[58:59]
	v_pk_add_f32 v[30:31], v[54:55], v[58:59] neg_lo:[0,1] neg_hi:[0,1]
	v_pk_add_f32 v[54:55], v[76:77], v[74:75]
	v_pk_mul_f32 v[50:51], v[10:11], v[50:51] op_sel_hi:[0,1] neg_lo:[1,0] neg_hi:[1,0]
	v_pk_add_f32 v[58:59], v[76:77], v[74:75] neg_lo:[0,1] neg_hi:[0,1]
	v_pk_fma_f32 v[34:35], v[10:11], v[34:35], v[50:51] op_sel_hi:[0,1,1] neg_lo:[1,0,0] neg_hi:[1,0,0]
	v_pk_add_f32 v[50:51], v[54:55], v[40:41]
	v_pk_add_f32 v[40:41], v[54:55], v[40:41] neg_lo:[0,1] neg_hi:[0,1]
	v_pk_add_f32 v[54:55], v[72:73], v[62:63]
	v_pk_add_f32 v[62:63], v[72:73], v[62:63] neg_lo:[0,1] neg_hi:[0,1]
	v_lshl_add_u32 v10, v13, 3, 0
	v_xor_b32_e32 v73, 0x80000000, v62
	v_mov_b32_e32 v72, v63
	v_pk_add_f32 v[62:63], v[50:51], v[54:55]
	v_pk_add_f32 v[54:55], v[50:51], v[54:55] neg_lo:[0,1] neg_hi:[0,1]
	v_pk_add_f32 v[50:51], v[58:59], v[66:67]
	v_pk_add_f32 v[58:59], v[58:59], v[66:67] neg_lo:[0,1] neg_hi:[0,1]
	v_pk_add_f32 v[66:67], v[64:65], v[34:35]
	v_pk_add_f32 v[34:35], v[64:65], v[34:35] neg_lo:[0,1] neg_hi:[0,1]
	v_pk_add_f32 v[74:75], v[40:41], v[72:73]
	v_xor_b32_e32 v65, 0x80000000, v34
	v_mov_b32_e32 v64, v35
	v_pk_add_f32 v[40:41], v[40:41], v[72:73] neg_lo:[0,1] neg_hi:[0,1]
	v_pk_add_f32 v[72:73], v[50:51], v[66:67]
	v_pk_add_f32 v[50:51], v[50:51], v[66:67] neg_lo:[0,1] neg_hi:[0,1]
	v_pk_add_f32 v[66:67], v[58:59], v[64:65]
	v_pk_add_f32 v[34:35], v[58:59], v[64:65] neg_lo:[0,1] neg_hi:[0,1]
	v_xor_b32_e32 v58, 0x80000000, v85
	v_mov_b32_e32 v59, v85
	v_pk_mul_f32 v[58:59], v[58:59], s[14:15]
	v_xor_b32_e32 v64, 0x80000000, v71
	v_pk_fma_f32 v[58:59], v[84:85], s[94:95], v[58:59] op_sel_hi:[0,1,1]
	ds_write_b64 v10, v[58:59]
	v_pk_fma_f32 v[58:59], v[14:15], s[90:91], v[14:15] op_sel:[1,0,0] op_sel_hi:[0,1,1]
	v_mov_b32_e32 v65, v71
	v_pk_mul_f32 v[64:65], v[58:59], v[64:65] op_sel:[1,0] op_sel_hi:[0,1]
	v_pk_fma_f32 v[64:65], v[58:59], v[70:71], v[64:65] op_sel_hi:[1,0,1]
	ds_write_b64 v10, v[64:65] offset:4224
	v_xor_b32_e32 v64, 0x80000000, v59
	v_mov_b32_e32 v65, v59
	v_pk_mul_f32 v[64:65], v[14:15], v[64:65] op_sel:[1,0] op_sel_hi:[0,1]
	v_pk_fma_f32 v[58:59], v[14:15], v[58:59], v[64:65] op_sel_hi:[1,0,1]
	v_xor_b32_e32 v64, 0x80000000, v89
	v_mov_b32_e32 v65, v89
	v_pk_mul_f32 v[64:65], v[58:59], v[64:65] op_sel:[1,0] op_sel_hi:[0,1]
	v_pk_fma_f32 v[64:65], v[58:59], v[88:89], v[64:65] op_sel_hi:[1,0,1]
	ds_write_b64 v10, v[64:65] offset:8448
	v_xor_b32_e32 v64, 0x80000000, v59
	v_mov_b32_e32 v65, v59
	v_pk_mul_f32 v[64:65], v[14:15], v[64:65] op_sel:[1,0] op_sel_hi:[0,1]
	v_pk_fma_f32 v[58:59], v[14:15], v[58:59], v[64:65] op_sel_hi:[1,0,1]
	v_xor_b32_e32 v64, 0x80000000, v63
	v_mov_b32_e32 v65, v63
	v_pk_mul_f32 v[64:65], v[58:59], v[64:65] op_sel:[1,0] op_sel_hi:[0,1]
	v_pk_fma_f32 v[62:63], v[58:59], v[62:63], v[64:65] op_sel_hi:[1,0,1]
	ds_write_b64 v10, v[62:63] offset:12672
	v_xor_b32_e32 v62, 0x80000000, v59
	v_mov_b32_e32 v63, v59
	v_pk_mul_f32 v[62:63], v[14:15], v[62:63] op_sel:[1,0] op_sel_hi:[0,1]
	v_pk_fma_f32 v[58:59], v[14:15], v[58:59], v[62:63] op_sel_hi:[1,0,1]
	v_xor_b32_e32 v62, 0x80000000, v79
	v_mov_b32_e32 v63, v79
	v_pk_mul_f32 v[62:63], v[58:59], v[62:63] op_sel:[1,0] op_sel_hi:[0,1]
	v_pk_fma_f32 v[62:63], v[58:59], v[78:79], v[62:63] op_sel_hi:[1,0,1]
	ds_write_b64 v10, v[62:63] offset:16896
	v_xor_b32_e32 v62, 0x80000000, v59
	v_mov_b32_e32 v63, v59
	v_pk_mul_f32 v[62:63], v[14:15], v[62:63] op_sel:[1,0] op_sel_hi:[0,1]
	v_pk_fma_f32 v[58:59], v[14:15], v[58:59], v[62:63] op_sel_hi:[1,0,1]
	v_xor_b32_e32 v62, 0x80000000, v61
	v_mov_b32_e32 v63, v61
	v_pk_mul_f32 v[62:63], v[58:59], v[62:63] op_sel:[1,0] op_sel_hi:[0,1]
	v_pk_fma_f32 v[60:61], v[58:59], v[60:61], v[62:63] op_sel_hi:[1,0,1]
	ds_write_b64 v10, v[60:61] offset:21120
	v_xor_b32_e32 v60, 0x80000000, v59
	v_mov_b32_e32 v61, v59
	v_pk_mul_f32 v[60:61], v[14:15], v[60:61] op_sel:[1,0] op_sel_hi:[0,1]
	v_pk_fma_f32 v[58:59], v[14:15], v[58:59], v[60:61] op_sel_hi:[1,0,1]
	v_xor_b32_e32 v60, 0x80000000, v83
	v_mov_b32_e32 v61, v83
	v_pk_mul_f32 v[60:61], v[60:61], v[58:59] op_sel:[0,1] op_sel_hi:[1,0]
	s_nop 0
	v_pk_fma_f32 v[60:61], v[82:83], v[58:59], v[60:61] op_sel_hi:[0,1,1]
	ds_write_b64 v10, v[60:61] offset:25344
	v_xor_b32_e32 v60, 0x80000000, v59
	v_mov_b32_e32 v61, v59
	v_pk_mul_f32 v[60:61], v[14:15], v[60:61] op_sel:[1,0] op_sel_hi:[0,1]
	v_pk_fma_f32 v[58:59], v[14:15], v[58:59], v[60:61] op_sel_hi:[1,0,1]
	v_xor_b32_e32 v60, 0x80000000, v73
	v_mov_b32_e32 v61, v73
	v_pk_mul_f32 v[60:61], v[60:61], v[58:59] op_sel:[0,1] op_sel_hi:[1,0]
	s_nop 0
	v_pk_fma_f32 v[60:61], v[72:73], v[58:59], v[60:61] op_sel_hi:[0,1,1]
	ds_write_b64 v10, v[60:61] offset:29568
	v_xor_b32_e32 v60, 0x80000000, v59
	v_mov_b32_e32 v61, v59
	v_pk_mul_f32 v[60:61], v[14:15], v[60:61] op_sel:[1,0] op_sel_hi:[0,1]
	v_pk_fma_f32 v[58:59], v[14:15], v[58:59], v[60:61] op_sel_hi:[1,0,1]
	v_xor_b32_e32 v60, 0x80000000, v45
	v_mov_b32_e32 v61, v45
	v_pk_mul_f32 v[60:61], v[60:61], v[58:59] op_sel:[0,1] op_sel_hi:[1,0]
	s_nop 0
	v_pk_fma_f32 v[44:45], v[44:45], v[58:59], v[60:61] op_sel_hi:[0,1,1]
	ds_write_b64 v10, v[44:45] offset:33792
	v_xor_b32_e32 v44, 0x80000000, v59
	v_mov_b32_e32 v45, v59
	v_pk_mul_f32 v[44:45], v[14:15], v[44:45] op_sel:[1,0] op_sel_hi:[0,1]
	v_pk_fma_f32 v[44:45], v[14:15], v[58:59], v[44:45] op_sel_hi:[1,0,1]
	v_xor_b32_e32 v58, 0x80000000, v69
	v_mov_b32_e32 v59, v69
	v_pk_mul_f32 v[58:59], v[58:59], v[44:45] op_sel:[0,1] op_sel_hi:[1,0]
	s_nop 0
	v_pk_fma_f32 v[58:59], v[68:69], v[44:45], v[58:59] op_sel_hi:[0,1,1]
	ds_write_b64 v10, v[58:59] offset:38016
	v_xor_b32_e32 v58, 0x80000000, v45
	v_mov_b32_e32 v59, v45
	v_pk_mul_f32 v[58:59], v[14:15], v[58:59] op_sel:[1,0] op_sel_hi:[0,1]
	v_pk_fma_f32 v[44:45], v[14:15], v[44:45], v[58:59] op_sel_hi:[1,0,1]
	v_xor_b32_e32 v58, 0x80000000, v49
	v_mov_b32_e32 v59, v49
	v_pk_mul_f32 v[58:59], v[58:59], v[44:45] op_sel:[0,1] op_sel_hi:[1,0]
	s_nop 0
	v_pk_fma_f32 v[48:49], v[48:49], v[44:45], v[58:59] op_sel_hi:[0,1,1]
	ds_write_b64 v10, v[48:49] offset:42240
	v_xor_b32_e32 v48, 0x80000000, v45
	v_mov_b32_e32 v49, v45
	v_pk_mul_f32 v[48:49], v[14:15], v[48:49] op_sel:[1,0] op_sel_hi:[0,1]
	v_pk_fma_f32 v[44:45], v[14:15], v[44:45], v[48:49] op_sel_hi:[1,0,1]
	v_xor_b32_e32 v48, 0x80000000, v75
	v_mov_b32_e32 v49, v75
	v_pk_mul_f32 v[48:49], v[48:49], v[44:45] op_sel:[0,1] op_sel_hi:[1,0]
	s_nop 0
	v_pk_fma_f32 v[48:49], v[74:75], v[44:45], v[48:49] op_sel_hi:[0,1,1]
	ds_write_b64 v10, v[48:49] offset:46464
	v_xor_b32_e32 v48, 0x80000000, v45
	v_mov_b32_e32 v49, v45
	v_pk_mul_f32 v[48:49], v[14:15], v[48:49] op_sel:[1,0] op_sel_hi:[0,1]
	v_pk_fma_f32 v[44:45], v[14:15], v[44:45], v[48:49] op_sel_hi:[1,0,1]
	v_xor_b32_e32 v48, 0x80000000, v39
	v_mov_b32_e32 v49, v39
	v_pk_mul_f32 v[48:49], v[48:49], v[44:45] op_sel:[0,1] op_sel_hi:[1,0]
	s_nop 0
	v_pk_fma_f32 v[38:39], v[38:39], v[44:45], v[48:49] op_sel_hi:[0,1,1]
	ds_write_b64 v10, v[38:39] offset:50688
	v_xor_b32_e32 v38, 0x80000000, v45
	v_mov_b32_e32 v39, v45
	v_pk_mul_f32 v[38:39], v[14:15], v[38:39] op_sel:[1,0] op_sel_hi:[0,1]
	v_pk_fma_f32 v[38:39], v[14:15], v[44:45], v[38:39] op_sel_hi:[1,0,1]
	v_xor_b32_e32 v44, 0x80000000, v57
	v_mov_b32_e32 v45, v57
	v_pk_mul_f32 v[44:45], v[44:45], v[38:39] op_sel:[0,1] op_sel_hi:[1,0]
	s_nop 0
	v_pk_fma_f32 v[44:45], v[56:57], v[38:39], v[44:45] op_sel_hi:[0,1,1]
	ds_write_b64 v10, v[44:45] offset:54912
	v_xor_b32_e32 v44, 0x80000000, v39
	v_mov_b32_e32 v45, v39
	v_pk_mul_f32 v[44:45], v[14:15], v[44:45] op_sel:[1,0] op_sel_hi:[0,1]
	v_pk_fma_f32 v[38:39], v[14:15], v[38:39], v[44:45] op_sel_hi:[1,0,1]
	v_xor_b32_e32 v44, 0x80000000, v43
	v_mov_b32_e32 v45, v43
	v_pk_mul_f32 v[44:45], v[44:45], v[38:39] op_sel:[0,1] op_sel_hi:[1,0]
	s_nop 0
	v_pk_fma_f32 v[42:43], v[42:43], v[38:39], v[44:45] op_sel_hi:[0,1,1]
	ds_write_b64 v10, v[42:43] offset:59136
	v_xor_b32_e32 v42, 0x80000000, v39
	v_mov_b32_e32 v43, v39
	v_pk_mul_f32 v[42:43], v[14:15], v[42:43] op_sel:[1,0] op_sel_hi:[0,1]
	v_pk_fma_f32 v[38:39], v[14:15], v[38:39], v[42:43] op_sel_hi:[1,0,1]
	v_xor_b32_e32 v42, 0x80000000, v67
	v_mov_b32_e32 v43, v67
	v_pk_mul_f32 v[42:43], v[42:43], v[38:39] op_sel:[0,1] op_sel_hi:[1,0]
	s_nop 0
	v_pk_fma_f32 v[42:43], v[66:67], v[38:39], v[42:43] op_sel_hi:[0,1,1]
	ds_write_b64 v10, v[42:43] offset:63360
	v_xor_b32_e32 v42, 0x80000000, v39
	v_mov_b32_e32 v43, v39
	v_pk_mul_f32 v[42:43], v[14:15], v[42:43] op_sel:[1,0] op_sel_hi:[0,1]
	v_pk_fma_f32 v[38:39], v[14:15], v[38:39], v[42:43] op_sel_hi:[1,0,1]
	v_xor_b32_e32 v42, 0x80000000, v29
	v_mov_b32_e32 v43, v29
	v_pk_mul_f32 v[42:43], v[42:43], v[38:39] op_sel:[0,1] op_sel_hi:[1,0]
	v_add_u32_e32 v13, 0x10800, v10
	v_pk_fma_f32 v[28:29], v[28:29], v[38:39], v[42:43] op_sel_hi:[0,1,1]
	ds_write_b64 v13, v[28:29]
	v_xor_b32_e32 v28, 0x80000000, v39
	v_mov_b32_e32 v29, v39
	v_pk_mul_f32 v[28:29], v[14:15], v[28:29] op_sel:[1,0] op_sel_hi:[0,1]
	v_pk_fma_f32 v[28:29], v[14:15], v[38:39], v[28:29] op_sel_hi:[1,0,1]
	v_xor_b32_e32 v38, 0x80000000, v53
	v_mov_b32_e32 v39, v53
	v_pk_mul_f32 v[38:39], v[38:39], v[28:29] op_sel:[0,1] op_sel_hi:[1,0]
	v_add_u32_e32 v13, 0x11880, v10
	v_pk_fma_f32 v[38:39], v[52:53], v[28:29], v[38:39] op_sel_hi:[0,1,1]
	ds_write_b64 v13, v[38:39]
	v_xor_b32_e32 v38, 0x80000000, v29
	v_mov_b32_e32 v39, v29
	v_pk_mul_f32 v[38:39], v[14:15], v[38:39] op_sel:[1,0] op_sel_hi:[0,1]
	v_pk_fma_f32 v[28:29], v[14:15], v[28:29], v[38:39] op_sel_hi:[1,0,1]
	v_xor_b32_e32 v38, 0x80000000, v33
	v_mov_b32_e32 v39, v33
	v_pk_mul_f32 v[38:39], v[38:39], v[28:29] op_sel:[0,1] op_sel_hi:[1,0]
	v_add_u32_e32 v13, 0x12900, v10
	v_pk_fma_f32 v[32:33], v[32:33], v[28:29], v[38:39] op_sel_hi:[0,1,1]
	ds_write_b64 v13, v[32:33]
	v_xor_b32_e32 v32, 0x80000000, v29
	v_mov_b32_e32 v33, v29
	v_pk_mul_f32 v[32:33], v[14:15], v[32:33] op_sel:[1,0] op_sel_hi:[0,1]
	v_pk_fma_f32 v[28:29], v[14:15], v[28:29], v[32:33] op_sel_hi:[1,0,1]
	v_xor_b32_e32 v32, 0x80000000, v55
	v_mov_b32_e32 v33, v55
	v_pk_mul_f32 v[32:33], v[32:33], v[28:29] op_sel:[0,1] op_sel_hi:[1,0]
	v_add_u32_e32 v13, 0x13980, v10
	v_pk_fma_f32 v[32:33], v[54:55], v[28:29], v[32:33] op_sel_hi:[0,1,1]
	ds_write_b64 v13, v[32:33]
	v_xor_b32_e32 v32, 0x80000000, v29
	v_mov_b32_e32 v33, v29
	v_pk_mul_f32 v[32:33], v[14:15], v[32:33] op_sel:[1,0] op_sel_hi:[0,1]
	v_pk_fma_f32 v[28:29], v[14:15], v[28:29], v[32:33] op_sel_hi:[1,0,1]
	v_xor_b32_e32 v32, 0x80000000, v25
	v_mov_b32_e32 v33, v25
	v_pk_mul_f32 v[32:33], v[32:33], v[28:29] op_sel:[0,1] op_sel_hi:[1,0]
	v_add_u32_e32 v13, 0x14a00, v10
	v_pk_fma_f32 v[24:25], v[24:25], v[28:29], v[32:33] op_sel_hi:[0,1,1]
	ds_write_b64 v13, v[24:25]
	v_xor_b32_e32 v24, 0x80000000, v29
	v_mov_b32_e32 v25, v29
	v_pk_mul_f32 v[24:25], v[14:15], v[24:25] op_sel:[1,0] op_sel_hi:[0,1]
	v_pk_fma_f32 v[24:25], v[14:15], v[28:29], v[24:25] op_sel_hi:[1,0,1]
	v_xor_b32_e32 v28, 0x80000000, v47
	v_mov_b32_e32 v29, v47
	v_pk_mul_f32 v[28:29], v[28:29], v[24:25] op_sel:[0,1] op_sel_hi:[1,0]
	v_add_u32_e32 v13, 0x15a80, v10
	v_pk_fma_f32 v[28:29], v[46:47], v[24:25], v[28:29] op_sel_hi:[0,1,1]
	ds_write_b64 v13, v[28:29]
	v_xor_b32_e32 v28, 0x80000000, v25
	v_mov_b32_e32 v29, v25
	v_pk_mul_f32 v[28:29], v[14:15], v[28:29] op_sel:[1,0] op_sel_hi:[0,1]
	v_pk_fma_f32 v[24:25], v[14:15], v[24:25], v[28:29] op_sel_hi:[1,0,1]
	v_xor_b32_e32 v28, 0x80000000, v27
	v_mov_b32_e32 v29, v27
	v_pk_mul_f32 v[28:29], v[28:29], v[24:25] op_sel:[0,1] op_sel_hi:[1,0]
	v_add_u32_e32 v13, 0x16b00, v10
	v_pk_fma_f32 v[26:27], v[26:27], v[24:25], v[28:29] op_sel_hi:[0,1,1]
	ds_write_b64 v13, v[26:27]
	v_xor_b32_e32 v26, 0x80000000, v25
	v_mov_b32_e32 v27, v25
	v_pk_mul_f32 v[26:27], v[14:15], v[26:27] op_sel:[1,0] op_sel_hi:[0,1]
	v_pk_fma_f32 v[24:25], v[14:15], v[24:25], v[26:27] op_sel_hi:[1,0,1]
	v_xor_b32_e32 v26, 0x80000000, v51
	v_mov_b32_e32 v27, v51
	v_pk_mul_f32 v[26:27], v[26:27], v[24:25] op_sel:[0,1] op_sel_hi:[1,0]
	v_add_u32_e32 v13, 0x17b80, v10
	v_pk_fma_f32 v[26:27], v[50:51], v[24:25], v[26:27] op_sel_hi:[0,1,1]
	ds_write_b64 v13, v[26:27]
	v_xor_b32_e32 v26, 0x80000000, v25
	v_mov_b32_e32 v27, v25
	v_pk_mul_f32 v[26:27], v[14:15], v[26:27] op_sel:[1,0] op_sel_hi:[0,1]
	v_pk_fma_f32 v[24:25], v[14:15], v[24:25], v[26:27] op_sel_hi:[1,0,1]
	v_xor_b32_e32 v26, 0x80000000, v21
	v_mov_b32_e32 v27, v21
	v_pk_mul_f32 v[26:27], v[26:27], v[24:25] op_sel:[0,1] op_sel_hi:[1,0]
	v_add_u32_e32 v13, 0x18c00, v10
	v_pk_fma_f32 v[20:21], v[20:21], v[24:25], v[26:27] op_sel_hi:[0,1,1]
	ds_write_b64 v13, v[20:21]
	v_xor_b32_e32 v20, 0x80000000, v25
	v_mov_b32_e32 v21, v25
	v_pk_mul_f32 v[20:21], v[14:15], v[20:21] op_sel:[1,0] op_sel_hi:[0,1]
	v_pk_fma_f32 v[20:21], v[14:15], v[24:25], v[20:21] op_sel_hi:[1,0,1]
	v_xor_b32_e32 v24, 0x80000000, v37
	v_mov_b32_e32 v25, v37
	v_pk_mul_f32 v[24:25], v[24:25], v[20:21] op_sel:[0,1] op_sel_hi:[1,0]
	v_add_u32_e32 v13, 0x19c80, v10
	v_pk_fma_f32 v[24:25], v[36:37], v[20:21], v[24:25] op_sel_hi:[0,1,1]
	ds_write_b64 v13, v[24:25]
	v_xor_b32_e32 v24, 0x80000000, v21
	v_mov_b32_e32 v25, v21
	v_pk_mul_f32 v[24:25], v[14:15], v[24:25] op_sel:[1,0] op_sel_hi:[0,1]
	v_pk_fma_f32 v[20:21], v[14:15], v[20:21], v[24:25] op_sel_hi:[1,0,1]
	v_xor_b32_e32 v24, 0x80000000, v23
	v_mov_b32_e32 v25, v23
	v_pk_mul_f32 v[24:25], v[24:25], v[20:21] op_sel:[0,1] op_sel_hi:[1,0]
	v_add_u32_e32 v13, 0x1ad00, v10
	v_pk_fma_f32 v[22:23], v[22:23], v[20:21], v[24:25] op_sel_hi:[0,1,1]
	ds_write_b64 v13, v[22:23]
	v_xor_b32_e32 v22, 0x80000000, v21
	v_mov_b32_e32 v23, v21
	v_pk_mul_f32 v[22:23], v[14:15], v[22:23] op_sel:[1,0] op_sel_hi:[0,1]
	v_pk_fma_f32 v[20:21], v[14:15], v[20:21], v[22:23] op_sel_hi:[1,0,1]
	v_xor_b32_e32 v22, 0x80000000, v41
	v_mov_b32_e32 v23, v41
	v_pk_mul_f32 v[22:23], v[22:23], v[20:21] op_sel:[0,1] op_sel_hi:[1,0]
	v_add_u32_e32 v13, 0x1bd80, v10
	v_pk_fma_f32 v[22:23], v[40:41], v[20:21], v[22:23] op_sel_hi:[0,1,1]
	ds_write_b64 v13, v[22:23]
	v_xor_b32_e32 v22, 0x80000000, v21
	v_mov_b32_e32 v23, v21
	v_pk_mul_f32 v[22:23], v[14:15], v[22:23] op_sel:[1,0] op_sel_hi:[0,1]
	v_pk_fma_f32 v[20:21], v[14:15], v[20:21], v[22:23] op_sel_hi:[1,0,1]
	v_xor_b32_e32 v22, 0x80000000, v17
	v_mov_b32_e32 v23, v17
	v_pk_mul_f32 v[22:23], v[22:23], v[20:21] op_sel:[0,1] op_sel_hi:[1,0]
	v_add_u32_e32 v13, 0x1ce00, v10
	v_pk_fma_f32 v[16:17], v[16:17], v[20:21], v[22:23] op_sel_hi:[0,1,1]
	ds_write_b64 v13, v[16:17]
	v_xor_b32_e32 v16, 0x80000000, v21
	v_mov_b32_e32 v17, v21
	v_pk_mul_f32 v[16:17], v[14:15], v[16:17] op_sel:[1,0] op_sel_hi:[0,1]
	v_pk_fma_f32 v[16:17], v[14:15], v[20:21], v[16:17] op_sel_hi:[1,0,1]
	v_xor_b32_e32 v20, 0x80000000, v31
	v_mov_b32_e32 v21, v31
	v_pk_mul_f32 v[20:21], v[20:21], v[16:17] op_sel:[0,1] op_sel_hi:[1,0]
	v_add_u32_e32 v13, 0x1de80, v10
	v_pk_fma_f32 v[20:21], v[30:31], v[16:17], v[20:21] op_sel_hi:[0,1,1]
	ds_write_b64 v13, v[20:21]
	v_xor_b32_e32 v20, 0x80000000, v17
	v_mov_b32_e32 v21, v17
	v_pk_mul_f32 v[20:21], v[14:15], v[20:21] op_sel:[1,0] op_sel_hi:[0,1]
	v_pk_fma_f32 v[16:17], v[14:15], v[16:17], v[20:21] op_sel_hi:[1,0,1]
	v_xor_b32_e32 v20, 0x80000000, v19
	v_mov_b32_e32 v21, v19
	v_pk_mul_f32 v[20:21], v[20:21], v[16:17] op_sel:[0,1] op_sel_hi:[1,0]
	v_add_u32_e32 v13, 0x1ef00, v10
	v_pk_fma_f32 v[18:19], v[18:19], v[16:17], v[20:21] op_sel_hi:[0,1,1]
	ds_write_b64 v13, v[18:19]
	v_xor_b32_e32 v18, 0x80000000, v17
	v_mov_b32_e32 v19, v17
	v_pk_mul_f32 v[18:19], v[14:15], v[18:19] op_sel:[1,0] op_sel_hi:[0,1]
	v_pk_fma_f32 v[14:15], v[14:15], v[16:17], v[18:19] op_sel_hi:[1,0,1]
	v_xor_b32_e32 v16, 0x80000000, v35
	v_mov_b32_e32 v17, v35
	v_pk_mul_f32 v[16:17], v[16:17], v[14:15] op_sel:[0,1] op_sel_hi:[1,0]
	v_add_u32_e32 v10, 0x1ff80, v10
	v_pk_fma_f32 v[14:15], v[34:35], v[14:15], v[16:17] op_sel_hi:[0,1,1]
	ds_write_b64 v10, v[14:15]
	v_mov_b32_e32 v10, v174
	v_mov_b32_e32 v13, v172
	s_waitcnt lgkmcnt(0)
	s_barrier
	v_mov_b32_e32 v14, v180
	v_xad_u32 v28, v13, 3, v10
	v_lshl_add_u32 v71, v28, 3, 0
	v_xad_u32 v28, v13, 4, v10
	v_lshl_add_u32 v70, v28, 3, 0
	v_xad_u32 v28, v13, 5, v10
	v_lshl_add_u32 v69, v28, 3, 0
	v_xad_u32 v28, v13, 6, v10
	v_lshl_add_u32 v68, v28, 3, 0
	v_xad_u32 v28, v13, 7, v10
	v_lshl_add_u32 v67, v28, 3, 0
	v_xad_u32 v28, v13, 8, v10
	v_lshl_add_u32 v28, v28, 3, 0
	v_add_u32_e32 v66, 0x800, v28
	v_xad_u32 v28, v13, 9, v10
	v_lshl_add_u32 v28, v28, 3, 0
	v_add_u32_e32 v65, 0x800, v28
	v_xad_u32 v28, v13, 10, v10
	v_lshl_add_u32 v28, v28, 3, 0
	v_add_u32_e32 v64, 0x800, v28
	v_xad_u32 v28, v13, 11, v10
	v_lshl_add_u32 v28, v28, 3, 0
	v_add_u32_e32 v16, v13, v10
	v_add_u32_e32 v63, 0x800, v28
	v_xad_u32 v28, v13, 12, v10
	v_mov_b32_e32 v15, v181
	v_lshl_add_u32 v74, v16, 3, 0
	v_lshl_add_u32 v28, v28, 3, 0
	ds_read2_b64 v[16:19], v74 offset1:16
	ds_read2_b64 v[38:41], v66 offset1:16
	v_add_u32_e32 v62, 0x800, v28
	v_xad_u32 v28, v13, 13, v10
	v_xad_u32 v20, v13, 1, v10
	v_lshl_add_u32 v28, v28, 3, 0
	v_lshl_add_u32 v73, v20, 3, 0
	v_xad_u32 v24, v13, 2, v10
	v_add_u32_e32 v61, 0x800, v28
	v_xad_u32 v28, v13, 14, v10
	v_xad_u32 v10, v13, 15, v10
	ds_read2_b64 v[20:23], v73 offset0:32 offset1:48
	ds_read2_b64 v[46:49], v65 offset0:32 offset1:48
	v_lshl_add_u32 v28, v28, 3, 0
	v_lshl_add_u32 v10, v10, 3, 0
	v_lshl_add_u32 v72, v24, 3, 0
	v_add_u32_e32 v60, 0x800, v28
	v_add_u32_e32 v13, 0x800, v10
	v_mov_b32_e32 v10, v1
	ds_read2_b64 v[24:27], v72 offset0:64 offset1:80
	ds_read2_b64 v[56:59], v71 offset0:96 offset1:112
	ds_read2_b64 v[76:79], v70 offset0:128 offset1:144
	ds_read2_b64 v[80:83], v69 offset0:160 offset1:176
	ds_read2_b64 v[84:87], v68 offset0:192 offset1:208
	ds_read2_b64 v[88:91], v67 offset0:224 offset1:240
	ds_read2_b64 v[52:55], v64 offset0:64 offset1:80
	ds_read2_b64 v[92:95], v63 offset0:96 offset1:112
	ds_read2_b64 v[96:99], v62 offset0:128 offset1:144
	ds_read2_b64 v[100:103], v61 offset0:160 offset1:176
	ds_read2_b64 v[104:107], v60 offset0:192 offset1:208
	ds_read2_b64 v[108:111], v13 offset0:224 offset1:240
	s_waitcnt lgkmcnt(14)
	v_pk_add_f32 v[112:113], v[16:17], v[38:39]
	v_pk_add_f32 v[38:39], v[16:17], v[38:39] neg_lo:[0,1] neg_hi:[0,1]
	v_pk_add_f32 v[16:17], v[18:19], v[40:41]
	v_pk_add_f32 v[18:19], v[18:19], v[40:41] neg_lo:[0,1] neg_hi:[0,1]
	v_mov_b32_e32 v28, v164
	v_mov_b32_e32 v30, v165
	v_mov_b32_e32 v32, v166
	v_mov_b32_e32 v10, v167
	v_mov_b32_e32 v36, v168
	v_mov_b32_e32 v34, v169
	v_mov_b32_e32 v44, v170
	v_xor_b32_e32 v40, 0x80000000, v19
	v_mov_b32_e32 v41, v18
	v_mov_b32_e32 v29, v171
	v_pk_mul_f32 v[40:41], v[40:41], v[44:45] op_sel_hi:[1,0] neg_lo:[0,1] neg_hi:[0,1]
	s_nop 0
	v_pk_fma_f32 v[42:43], v[18:19], v[28:29], v[40:41] op_sel_hi:[1,0,1]
	s_waitcnt lgkmcnt(12)
	v_pk_add_f32 v[18:19], v[20:21], v[46:47]
	v_pk_add_f32 v[20:21], v[20:21], v[46:47] neg_lo:[0,1] neg_hi:[0,1]
	s_nop 0
	v_xor_b32_e32 v40, 0x80000000, v21
	v_mov_b32_e32 v41, v20
	v_pk_mul_f32 v[40:41], v[40:41], v[34:35] op_sel_hi:[1,0] neg_lo:[0,1] neg_hi:[0,1]
	s_nop 0
	v_pk_fma_f32 v[46:47], v[20:21], v[30:31], v[40:41] op_sel_hi:[1,0,1]
	v_pk_add_f32 v[20:21], v[22:23], v[48:49]
	v_pk_add_f32 v[22:23], v[22:23], v[48:49] neg_lo:[0,1] neg_hi:[0,1]
	s_nop 0
	v_xor_b32_e32 v40, 0x80000000, v23
	v_mov_b32_e32 v41, v22
	v_pk_mul_f32 v[40:41], v[40:41], v[36:37] op_sel_hi:[1,0] neg_lo:[0,1] neg_hi:[0,1]
	s_nop 0
	v_pk_fma_f32 v[50:51], v[22:23], v[32:33], v[40:41] op_sel_hi:[1,0,1]
	s_waitcnt lgkmcnt(5)
	v_pk_add_f32 v[22:23], v[24:25], v[52:53]
	v_pk_add_f32 v[24:25], v[24:25], v[52:53] neg_lo:[0,1] neg_hi:[0,1]
	s_nop 0
	v_xor_b32_e32 v40, 0x80000000, v25
	v_mov_b32_e32 v41, v24
	v_pk_mul_f32 v[40:41], v[40:41], v[10:11] op_sel_hi:[1,0] neg_lo:[0,1] neg_hi:[0,1]
	s_nop 0
	v_pk_fma_f32 v[52:53], v[24:25], v[10:11], v[40:41] op_sel_hi:[1,0,1]
	v_pk_add_f32 v[24:25], v[26:27], v[54:55]
	v_pk_add_f32 v[26:27], v[26:27], v[54:55] neg_lo:[0,1] neg_hi:[0,1]
	s_nop 0
	v_pk_mul_f32 v[40:41], v[26:27], v[36:37] op_sel_hi:[1,0]
	v_xor_b32_e32 v48, 0x80000000, v27
	v_mov_b32_e32 v49, v26
	v_pk_fma_f32 v[54:55], v[48:49], v[32:33], v[40:41] op_sel_hi:[1,0,1] neg_lo:[0,1,0] neg_hi:[0,1,0]
	s_waitcnt lgkmcnt(4)
	v_pk_add_f32 v[40:41], v[56:57], v[92:93] neg_lo:[0,1] neg_hi:[0,1]
	v_pk_add_f32 v[26:27], v[56:57], v[92:93]
	v_pk_mul_f32 v[48:49], v[40:41], v[34:35] op_sel_hi:[1,0]
	v_xor_b32_e32 v56, 0x80000000, v41
	v_mov_b32_e32 v57, v40
	v_pk_fma_f32 v[56:57], v[56:57], v[30:31], v[48:49] op_sel_hi:[1,0,1] neg_lo:[0,1,0] neg_hi:[0,1,0]
	v_pk_add_f32 v[48:49], v[58:59], v[94:95] neg_lo:[0,1] neg_hi:[0,1]
	v_pk_add_f32 v[40:41], v[58:59], v[94:95]
	v_pk_mul_f32 v[58:59], v[48:49], v[44:45] op_sel_hi:[1,0]
	v_xor_b32_e32 v92, 0x80000000, v49
	v_mov_b32_e32 v93, v48
	s_waitcnt lgkmcnt(3)
	v_pk_add_f32 v[48:49], v[76:77], v[96:97]
	v_pk_add_f32 v[76:77], v[76:77], v[96:97] neg_lo:[0,1] neg_hi:[0,1]
	v_pk_fma_f32 v[58:59], v[92:93], v[28:29], v[58:59] op_sel_hi:[1,0,1] neg_lo:[0,1,0] neg_hi:[0,1,0]
	v_xor_b32_e32 v93, 0x80000000, v76
	v_mov_b32_e32 v92, v77
	v_pk_add_f32 v[76:77], v[78:79], v[98:99]
	v_pk_add_f32 v[78:79], v[78:79], v[98:99] neg_lo:[0,1] neg_hi:[0,1]
	s_nop 0
	v_pk_mul_f32 v[94:95], v[78:79], v[44:45] op_sel_hi:[1,0] neg_lo:[0,1] neg_hi:[0,1]
	v_xor_b32_e32 v96, 0x80000000, v79
	v_mov_b32_e32 v97, v78
	v_pk_fma_f32 v[78:79], v[96:97], v[28:29], v[94:95] op_sel_hi:[1,0,1] neg_lo:[0,1,0] neg_hi:[0,1,0]
	s_waitcnt lgkmcnt(2)
	v_pk_add_f32 v[94:95], v[80:81], v[100:101]
	v_pk_add_f32 v[80:81], v[80:81], v[100:101] neg_lo:[0,1] neg_hi:[0,1]
	s_nop 0
	v_pk_mul_f32 v[96:97], v[80:81], v[34:35] op_sel_hi:[1,0] neg_lo:[0,1] neg_hi:[0,1]
	v_xor_b32_e32 v98, 0x80000000, v81
	v_mov_b32_e32 v99, v80
	v_pk_fma_f32 v[80:81], v[98:99], v[30:31], v[96:97] op_sel_hi:[1,0,1] neg_lo:[0,1,0] neg_hi:[0,1,0]
	v_pk_add_f32 v[96:97], v[82:83], v[102:103]
	v_pk_add_f32 v[82:83], v[82:83], v[102:103] neg_lo:[0,1] neg_hi:[0,1]
	s_nop 0
	v_pk_mul_f32 v[98:99], v[82:83], v[36:37] op_sel_hi:[1,0] neg_lo:[0,1] neg_hi:[0,1]
	v_xor_b32_e32 v100, 0x80000000, v83
	v_mov_b32_e32 v101, v82
	v_pk_fma_f32 v[82:83], v[100:101], v[32:33], v[98:99] op_sel_hi:[1,0,1] neg_lo:[0,1,0] neg_hi:[0,1,0]
	s_waitcnt lgkmcnt(1)
	v_pk_add_f32 v[98:99], v[84:85], v[104:105]
	v_pk_add_f32 v[84:85], v[84:85], v[104:105] neg_lo:[0,1] neg_hi:[0,1]
	s_nop 0
	v_xor_b32_e32 v100, 0x80000000, v85
	v_mov_b32_e32 v101, v84
	v_pk_mul_f32 v[100:101], v[100:101], v[10:11] op_sel_hi:[1,0] neg_lo:[0,1] neg_hi:[0,1]
	s_nop 0
	v_pk_fma_f32 v[84:85], v[84:85], v[10:11], v[100:101] op_sel_hi:[1,0,1] neg_lo:[0,1,0] neg_hi:[0,1,0]
	v_pk_add_f32 v[100:101], v[86:87], v[106:107]
	v_pk_add_f32 v[86:87], v[86:87], v[106:107] neg_lo:[0,1] neg_hi:[0,1]
	s_nop 0
	v_xor_b32_e32 v102, 0x80000000, v87
	v_mov_b32_e32 v103, v86
	v_pk_mul_f32 v[36:37], v[102:103], v[36:37] op_sel_hi:[1,0] neg_lo:[0,1] neg_hi:[0,1]
	s_nop 0
	v_pk_fma_f32 v[86:87], v[86:87], v[32:33], v[36:37] op_sel_hi:[1,0,1] neg_lo:[0,1,0] neg_hi:[0,1,0]
	s_waitcnt lgkmcnt(0)
	v_pk_add_f32 v[36:37], v[88:89], v[108:109] neg_lo:[0,1] neg_hi:[0,1]
	v_pk_add_f32 v[32:33], v[88:89], v[108:109]
	v_xor_b32_e32 v88, 0x80000000, v37
	v_mov_b32_e32 v89, v36
	v_pk_mul_f32 v[88:89], v[88:89], v[34:35] op_sel_hi:[1,0] neg_lo:[0,1] neg_hi:[0,1]
	s_nop 0
	v_pk_fma_f32 v[88:89], v[36:37], v[30:31], v[88:89] op_sel_hi:[1,0,1] neg_lo:[0,1,0] neg_hi:[0,1,0]
	v_pk_add_f32 v[36:37], v[90:91], v[110:111]
	v_pk_add_f32 v[90:91], v[90:91], v[110:111] neg_lo:[0,1] neg_hi:[0,1]
	s_nop 0
	v_xor_b32_e32 v102, 0x80000000, v91
	v_mov_b32_e32 v103, v90
	v_pk_mul_f32 v[44:45], v[102:103], v[44:45] op_sel_hi:[1,0] neg_lo:[0,1] neg_hi:[0,1]
	s_nop 0
	v_pk_fma_f32 v[90:91], v[90:91], v[28:29], v[44:45] op_sel_hi:[1,0,1] neg_lo:[0,1,0] neg_hi:[0,1,0]
	v_pk_add_f32 v[44:45], v[16:17], v[76:77]
	v_pk_add_f32 v[16:17], v[16:17], v[76:77] neg_lo:[0,1] neg_hi:[0,1]
	v_pk_add_f32 v[28:29], v[112:113], v[48:49]
	v_xor_b32_e32 v76, 0x80000000, v17
	v_mov_b32_e32 v77, v16
	v_pk_mul_f32 v[76:77], v[76:77], v[34:35] op_sel_hi:[1,0] neg_lo:[0,1] neg_hi:[0,1]
	v_pk_add_f32 v[48:49], v[112:113], v[48:49] neg_lo:[0,1] neg_hi:[0,1]
	v_pk_fma_f32 v[76:77], v[16:17], v[30:31], v[76:77] op_sel_hi:[1,0,1]
	v_pk_add_f32 v[16:17], v[18:19], v[94:95]
	v_pk_add_f32 v[18:19], v[18:19], v[94:95] neg_lo:[0,1] neg_hi:[0,1]
	s_nop 0
	v_xor_b32_e32 v94, 0x80000000, v19
	v_mov_b32_e32 v95, v18
	v_pk_mul_f32 v[94:95], v[94:95], v[10:11] op_sel_hi:[1,0] neg_lo:[0,1] neg_hi:[0,1]
	s_nop 0
	v_pk_fma_f32 v[18:19], v[18:19], v[10:11], v[94:95] op_sel_hi:[1,0,1]
	v_pk_add_f32 v[94:95], v[20:21], v[96:97]
	v_pk_add_f32 v[20:21], v[20:21], v[96:97] neg_lo:[0,1] neg_hi:[0,1]
	s_nop 0
	v_pk_mul_f32 v[96:97], v[20:21], v[34:35] op_sel_hi:[1,0]
	v_xor_b32_e32 v102, 0x80000000, v21
	v_mov_b32_e32 v103, v20
	v_pk_add_f32 v[20:21], v[22:23], v[98:99]
	v_pk_add_f32 v[22:23], v[22:23], v[98:99] neg_lo:[0,1] neg_hi:[0,1]
	v_pk_fma_f32 v[96:97], v[102:103], v[30:31], v[96:97] op_sel_hi:[1,0,1] neg_lo:[0,1,0] neg_hi:[0,1,0]
	v_xor_b32_e32 v99, 0x80000000, v22
	v_mov_b32_e32 v98, v23
	v_pk_add_f32 v[22:23], v[24:25], v[100:101]
	v_pk_add_f32 v[24:25], v[24:25], v[100:101] neg_lo:[0,1] neg_hi:[0,1]
	s_nop 0
	v_pk_mul_f32 v[100:101], v[24:25], v[34:35] op_sel_hi:[1,0] neg_lo:[0,1] neg_hi:[0,1]
	v_xor_b32_e32 v102, 0x80000000, v25
	v_mov_b32_e32 v103, v24
	v_pk_add_f32 v[24:25], v[26:27], v[32:33]
	v_pk_add_f32 v[26:27], v[26:27], v[32:33] neg_lo:[0,1] neg_hi:[0,1]
	v_pk_fma_f32 v[100:101], v[102:103], v[30:31], v[100:101] op_sel_hi:[1,0,1] neg_lo:[0,1,0] neg_hi:[0,1,0]
	v_xor_b32_e32 v32, 0x80000000, v27
	v_mov_b32_e32 v33, v26
	v_pk_mul_f32 v[32:33], v[32:33], v[10:11] op_sel_hi:[1,0] neg_lo:[0,1] neg_hi:[0,1]
	v_pk_add_f32 v[102:103], v[28:29], v[20:21] neg_lo:[0,1] neg_hi:[0,1]
	v_pk_fma_f32 v[26:27], v[26:27], v[10:11], v[32:33] op_sel_hi:[1,0,1] neg_lo:[0,1,0] neg_hi:[0,1,0]
	v_pk_add_f32 v[32:33], v[40:41], v[36:37]
	v_pk_add_f32 v[36:37], v[40:41], v[36:37] neg_lo:[0,1] neg_hi:[0,1]
	s_nop 0
	v_xor_b32_e32 v40, 0x80000000, v37
	v_mov_b32_e32 v41, v36
	v_pk_mul_f32 v[40:41], v[40:41], v[34:35] op_sel_hi:[1,0] neg_lo:[0,1] neg_hi:[0,1]
	s_nop 0
	v_pk_fma_f32 v[40:41], v[36:37], v[30:31], v[40:41] op_sel_hi:[1,0,1] neg_lo:[0,1,0] neg_hi:[0,1,0]
	v_pk_add_f32 v[36:37], v[28:29], v[20:21]
	v_pk_add_f32 v[20:21], v[44:45], v[22:23]
	v_pk_add_f32 v[22:23], v[44:45], v[22:23] neg_lo:[0,1] neg_hi:[0,1]
	s_nop 0
	v_xor_b32_e32 v28, 0x80000000, v23
	v_mov_b32_e32 v29, v22
	v_pk_mul_f32 v[28:29], v[28:29], v[10:11] op_sel_hi:[1,0] neg_lo:[0,1] neg_hi:[0,1]
	s_nop 0
	v_pk_fma_f32 v[22:23], v[22:23], v[10:11], v[28:29] op_sel_hi:[1,0,1]
	v_pk_add_f32 v[28:29], v[16:17], v[24:25]
	v_pk_add_f32 v[16:17], v[16:17], v[24:25] neg_lo:[0,1] neg_hi:[0,1]
	s_nop 0
	v_xor_b32_e32 v25, 0x80000000, v16
	v_mov_b32_e32 v24, v17
	v_pk_add_f32 v[16:17], v[94:95], v[32:33]
	v_pk_add_f32 v[32:33], v[94:95], v[32:33] neg_lo:[0,1] neg_hi:[0,1]
	s_nop 0
	v_xor_b32_e32 v44, 0x80000000, v33
	v_mov_b32_e32 v45, v32
	v_pk_mul_f32 v[44:45], v[44:45], v[10:11] op_sel_hi:[1,0] neg_lo:[0,1] neg_hi:[0,1]
	s_nop 0
	v_pk_fma_f32 v[32:33], v[32:33], v[10:11], v[44:45] op_sel_hi:[1,0,1] neg_lo:[0,1,0] neg_hi:[0,1,0]
	v_pk_add_f32 v[44:45], v[36:37], v[28:29]
	v_pk_add_f32 v[36:37], v[36:37], v[28:29] neg_lo:[0,1] neg_hi:[0,1]
	v_pk_add_f32 v[28:29], v[20:21], v[16:17]
	v_pk_add_f32 v[16:17], v[20:21], v[16:17] neg_lo:[0,1] neg_hi:[0,1]
	v_pk_add_f32 v[94:95], v[44:45], v[28:29]
	v_xor_b32_e32 v21, 0x80000000, v16
	v_mov_b32_e32 v20, v17
	v_pk_add_f32 v[16:17], v[102:103], v[24:25]
	v_pk_add_f32 v[102:103], v[102:103], v[24:25] neg_lo:[0,1] neg_hi:[0,1]
	v_pk_add_f32 v[24:25], v[22:23], v[32:33]
	v_pk_add_f32 v[22:23], v[22:23], v[32:33] neg_lo:[0,1] neg_hi:[0,1]
	v_pk_add_f32 v[28:29], v[44:45], v[28:29] neg_lo:[0,1] neg_hi:[0,1]
	v_xor_b32_e32 v33, 0x80000000, v22
	v_mov_b32_e32 v32, v23
	v_pk_add_f32 v[22:23], v[48:49], v[98:99]
	v_pk_add_f32 v[98:99], v[48:49], v[98:99] neg_lo:[0,1] neg_hi:[0,1]
	v_pk_add_f32 v[48:49], v[76:77], v[100:101] neg_lo:[0,1] neg_hi:[0,1]
	v_pk_add_f32 v[44:45], v[36:37], v[20:21]
	v_pk_add_f32 v[20:21], v[36:37], v[20:21] neg_lo:[0,1] neg_hi:[0,1]
	v_pk_add_f32 v[104:105], v[16:17], v[24:25]
	v_pk_add_f32 v[24:25], v[16:17], v[24:25] neg_lo:[0,1] neg_hi:[0,1]
	v_pk_add_f32 v[36:37], v[102:103], v[32:33]
	v_pk_add_f32 v[16:17], v[102:103], v[32:33] neg_lo:[0,1] neg_hi:[0,1]
	v_pk_add_f32 v[32:33], v[76:77], v[100:101]
	v_xor_b32_e32 v76, 0x80000000, v49
	v_mov_b32_e32 v77, v48
	v_pk_mul_f32 v[76:77], v[10:11], v[76:77] op_sel_hi:[0,1] neg_lo:[1,0] neg_hi:[1,0]
	v_pk_fma_f32 v[76:77], v[10:11], v[48:49], v[76:77] op_sel_hi:[0,1,1]
	v_pk_add_f32 v[48:49], v[18:19], v[26:27]
	v_pk_add_f32 v[18:19], v[18:19], v[26:27] neg_lo:[0,1] neg_hi:[0,1]
	s_nop 0
	v_xor_b32_e32 v27, 0x80000000, v18
	v_mov_b32_e32 v26, v19
	v_pk_add_f32 v[18:19], v[96:97], v[40:41]
	v_pk_add_f32 v[40:41], v[96:97], v[40:41] neg_lo:[0,1] neg_hi:[0,1]
	s_nop 0
	v_xor_b32_e32 v96, 0x80000000, v41
	v_mov_b32_e32 v97, v40
	v_pk_mul_f32 v[96:97], v[10:11], v[96:97] op_sel_hi:[0,1] neg_lo:[1,0] neg_hi:[1,0]
	v_pk_fma_f32 v[40:41], v[10:11], v[40:41], v[96:97] op_sel_hi:[0,1,1] neg_lo:[1,0,0] neg_hi:[1,0,0]
	v_pk_add_f32 v[96:97], v[22:23], v[48:49]
	v_pk_add_f32 v[22:23], v[22:23], v[48:49] neg_lo:[0,1] neg_hi:[0,1]
	v_pk_add_f32 v[48:49], v[32:33], v[18:19]
	v_pk_add_f32 v[18:19], v[32:33], v[18:19] neg_lo:[0,1] neg_hi:[0,1]
	v_pk_add_f32 v[102:103], v[96:97], v[48:49]
	v_xor_b32_e32 v101, 0x80000000, v18
	v_mov_b32_e32 v100, v19
	v_pk_add_f32 v[32:33], v[96:97], v[48:49] neg_lo:[0,1] neg_hi:[0,1]
	v_pk_add_f32 v[18:19], v[98:99], v[26:27]
	v_pk_add_f32 v[96:97], v[98:99], v[26:27] neg_lo:[0,1] neg_hi:[0,1]
	v_pk_add_f32 v[26:27], v[76:77], v[40:41]
	v_pk_add_f32 v[40:41], v[76:77], v[40:41] neg_lo:[0,1] neg_hi:[0,1]
	v_pk_add_f32 v[98:99], v[18:19], v[26:27]
	v_xor_b32_e32 v77, 0x80000000, v40
	v_mov_b32_e32 v76, v41
	v_pk_add_f32 v[26:27], v[18:19], v[26:27] neg_lo:[0,1] neg_hi:[0,1]
	v_pk_add_f32 v[40:41], v[96:97], v[76:77]
	v_pk_add_f32 v[18:19], v[96:97], v[76:77] neg_lo:[0,1] neg_hi:[0,1]
	v_pk_add_f32 v[76:77], v[38:39], v[92:93]
	v_pk_add_f32 v[92:93], v[38:39], v[92:93] neg_lo:[0,1] neg_hi:[0,1]
	v_pk_add_f32 v[38:39], v[42:43], v[78:79]
	v_pk_add_f32 v[42:43], v[42:43], v[78:79] neg_lo:[0,1] neg_hi:[0,1]
	v_pk_add_f32 v[48:49], v[22:23], v[100:101]
	v_xor_b32_e32 v78, 0x80000000, v43
	v_mov_b32_e32 v79, v42
	v_pk_mul_f32 v[78:79], v[34:35], v[78:79] op_sel_hi:[0,1] neg_lo:[1,0] neg_hi:[1,0]
	v_pk_fma_f32 v[42:43], v[30:31], v[42:43], v[78:79] op_sel_hi:[0,1,1]
	v_pk_add_f32 v[78:79], v[46:47], v[80:81]
	v_pk_add_f32 v[46:47], v[46:47], v[80:81] neg_lo:[0,1] neg_hi:[0,1]
	v_pk_add_f32 v[22:23], v[22:23], v[100:101] neg_lo:[0,1] neg_hi:[0,1]
	v_xor_b32_e32 v80, 0x80000000, v47
	v_mov_b32_e32 v81, v46
	v_pk_mul_f32 v[80:81], v[10:11], v[80:81] op_sel_hi:[0,1] neg_lo:[1,0] neg_hi:[1,0]
	v_pk_fma_f32 v[80:81], v[10:11], v[46:47], v[80:81] op_sel_hi:[0,1,1]
	v_pk_add_f32 v[46:47], v[50:51], v[82:83]
	v_pk_add_f32 v[50:51], v[50:51], v[82:83] neg_lo:[0,1] neg_hi:[0,1]
	s_nop 0
	v_xor_b32_e32 v82, 0x80000000, v51
	v_mov_b32_e32 v83, v50
	v_pk_mul_f32 v[82:83], v[30:31], v[82:83] op_sel_hi:[0,1] neg_lo:[1,0] neg_hi:[1,0]
	v_pk_fma_f32 v[50:51], v[34:35], v[50:51], v[82:83] op_sel_hi:[0,1,1]
	v_pk_add_f32 v[82:83], v[52:53], v[84:85]
	v_pk_add_f32 v[52:53], v[52:53], v[84:85] neg_lo:[0,1] neg_hi:[0,1]
	s_nop 0
	v_xor_b32_e32 v85, 0x80000000, v52
	v_mov_b32_e32 v84, v53
	v_pk_add_f32 v[52:53], v[54:55], v[86:87]
	v_pk_add_f32 v[54:55], v[54:55], v[86:87] neg_lo:[0,1] neg_hi:[0,1]
	s_nop 0
	v_xor_b32_e32 v86, 0x80000000, v55
	v_mov_b32_e32 v87, v54
	v_pk_mul_f32 v[86:87], v[30:31], v[86:87] op_sel_hi:[0,1] neg_lo:[1,0] neg_hi:[1,0]
	v_pk_fma_f32 v[54:55], v[34:35], v[54:55], v[86:87] op_sel_hi:[0,1,1] neg_lo:[1,0,0] neg_hi:[1,0,0]
	v_pk_add_f32 v[86:87], v[56:57], v[88:89]
	v_pk_add_f32 v[56:57], v[56:57], v[88:89] neg_lo:[0,1] neg_hi:[0,1]
	s_nop 0
	v_xor_b32_e32 v88, 0x80000000, v57
	v_mov_b32_e32 v89, v56
	v_pk_mul_f32 v[88:89], v[10:11], v[88:89] op_sel_hi:[0,1] neg_lo:[1,0] neg_hi:[1,0]
	v_pk_fma_f32 v[56:57], v[10:11], v[56:57], v[88:89] op_sel_hi:[0,1,1] neg_lo:[1,0,0] neg_hi:[1,0,0]
	v_pk_add_f32 v[88:89], v[58:59], v[90:91]
	v_pk_add_f32 v[58:59], v[58:59], v[90:91] neg_lo:[0,1] neg_hi:[0,1]
	s_nop 0
	v_xor_b32_e32 v90, 0x80000000, v59
	v_mov_b32_e32 v91, v58
	v_pk_mul_f32 v[34:35], v[34:35], v[90:91] op_sel_hi:[0,1] neg_lo:[1,0] neg_hi:[1,0]
	v_pk_fma_f32 v[34:35], v[30:31], v[58:59], v[34:35] op_sel_hi:[0,1,1] neg_lo:[1,0,0] neg_hi:[1,0,0]
	v_pk_add_f32 v[30:31], v[76:77], v[82:83]
	v_pk_add_f32 v[58:59], v[76:77], v[82:83] neg_lo:[0,1] neg_hi:[0,1]
	v_pk_add_f32 v[76:77], v[52:53], v[38:39]
	v_pk_add_f32 v[38:39], v[38:39], v[52:53] neg_lo:[0,1] neg_hi:[0,1]
	s_nop 0
	v_xor_b32_e32 v52, 0x80000000, v39
	v_mov_b32_e32 v53, v38
	v_pk_mul_f32 v[52:53], v[10:11], v[52:53] op_sel_hi:[0,1] neg_lo:[1,0] neg_hi:[1,0]
	v_pk_fma_f32 v[52:53], v[10:11], v[38:39], v[52:53] op_sel_hi:[0,1,1]
	v_pk_add_f32 v[38:39], v[78:79], v[86:87]
	v_pk_add_f32 v[78:79], v[78:79], v[86:87] neg_lo:[0,1] neg_hi:[0,1]
	s_nop 0
	v_xor_b32_e32 v83, 0x80000000, v78
	v_mov_b32_e32 v82, v79
	v_pk_add_f32 v[78:79], v[46:47], v[88:89]
	v_pk_add_f32 v[46:47], v[46:47], v[88:89] neg_lo:[0,1] neg_hi:[0,1]
	v_pk_add_f32 v[88:89], v[76:77], v[78:79]
	v_xor_b32_e32 v86, 0x80000000, v47
	v_mov_b32_e32 v87, v46
	v_pk_mul_f32 v[86:87], v[10:11], v[86:87] op_sel_hi:[0,1] neg_lo:[1,0] neg_hi:[1,0]
	v_pk_fma_f32 v[46:47], v[10:11], v[46:47], v[86:87] op_sel_hi:[0,1,1] neg_lo:[1,0,0] neg_hi:[1,0,0]
	v_pk_add_f32 v[86:87], v[30:31], v[38:39]
	v_pk_add_f32 v[30:31], v[30:31], v[38:39] neg_lo:[0,1] neg_hi:[0,1]
	v_pk_add_f32 v[38:39], v[76:77], v[78:79] neg_lo:[0,1] neg_hi:[0,1]
	v_pk_add_f32 v[78:79], v[86:87], v[88:89] neg_lo:[0,1] neg_hi:[0,1]
	v_xor_b32_e32 v77, 0x80000000, v38
	v_mov_b32_e32 v76, v39
	v_pk_add_f32 v[90:91], v[30:31], v[76:77]
	v_pk_add_f32 v[38:39], v[30:31], v[76:77] neg_lo:[0,1] neg_hi:[0,1]
	v_pk_add_f32 v[76:77], v[52:53], v[46:47]
	v_pk_add_f32 v[46:47], v[52:53], v[46:47] neg_lo:[0,1] neg_hi:[0,1]
	v_pk_add_f32 v[30:31], v[58:59], v[82:83]
	v_pk_add_f32 v[58:59], v[58:59], v[82:83] neg_lo:[0,1] neg_hi:[0,1]
	v_xor_b32_e32 v53, 0x80000000, v46
	v_mov_b32_e32 v52, v47
	v_pk_add_f32 v[82:83], v[30:31], v[76:77]
	v_pk_add_f32 v[46:47], v[30:31], v[76:77] neg_lo:[0,1] neg_hi:[0,1]
	v_pk_add_f32 v[76:77], v[58:59], v[52:53]
	v_pk_add_f32 v[30:31], v[58:59], v[52:53] neg_lo:[0,1] neg_hi:[0,1]
	v_pk_add_f32 v[52:53], v[92:93], v[84:85]
	v_pk_add_f32 v[58:59], v[92:93], v[84:85] neg_lo:[0,1] neg_hi:[0,1]
	v_pk_add_f32 v[84:85], v[54:55], v[42:43]
	v_pk_add_f32 v[42:43], v[42:43], v[54:55] neg_lo:[0,1] neg_hi:[0,1]
	v_pk_add_f32 v[86:87], v[86:87], v[88:89]
	v_xor_b32_e32 v54, 0x80000000, v43
	v_mov_b32_e32 v55, v42
	v_pk_mul_f32 v[54:55], v[10:11], v[54:55] op_sel_hi:[0,1] neg_lo:[1,0] neg_hi:[1,0]
	v_pk_fma_f32 v[54:55], v[10:11], v[42:43], v[54:55] op_sel_hi:[0,1,1]
	v_pk_add_f32 v[42:43], v[80:81], v[56:57]
	v_pk_add_f32 v[56:57], v[80:81], v[56:57] neg_lo:[0,1] neg_hi:[0,1]
	v_xor_b32_e32 v88, 0x80000000, v87
	v_xor_b32_e32 v81, 0x80000000, v56
	v_mov_b32_e32 v80, v57
	v_pk_add_f32 v[56:57], v[50:51], v[34:35]
	v_pk_add_f32 v[34:35], v[50:51], v[34:35] neg_lo:[0,1] neg_hi:[0,1]
	v_mov_b32_e32 v89, v87
	v_xor_b32_e32 v50, 0x80000000, v35
	v_mov_b32_e32 v51, v34
	v_pk_mul_f32 v[50:51], v[10:11], v[50:51] op_sel_hi:[0,1] neg_lo:[1,0] neg_hi:[1,0]
	v_pk_fma_f32 v[34:35], v[10:11], v[34:35], v[50:51] op_sel_hi:[0,1,1] neg_lo:[1,0,0] neg_hi:[1,0,0]
	v_pk_add_f32 v[50:51], v[52:53], v[42:43]
	v_pk_add_f32 v[42:43], v[52:53], v[42:43] neg_lo:[0,1] neg_hi:[0,1]
	v_pk_add_f32 v[52:53], v[84:85], v[56:57]
	v_pk_add_f32 v[56:57], v[84:85], v[56:57] neg_lo:[0,1] neg_hi:[0,1]
	s_nop 0
	v_xor_b32_e32 v85, 0x80000000, v56
	v_mov_b32_e32 v84, v57
	v_pk_add_f32 v[56:57], v[50:51], v[52:53]
	v_pk_add_f32 v[50:51], v[50:51], v[52:53] neg_lo:[0,1] neg_hi:[0,1]
	v_pk_add_f32 v[52:53], v[42:43], v[84:85]
	v_pk_add_f32 v[42:43], v[42:43], v[84:85] neg_lo:[0,1] neg_hi:[0,1]
	v_pk_add_f32 v[84:85], v[58:59], v[80:81]
	v_pk_add_f32 v[58:59], v[58:59], v[80:81] neg_lo:[0,1] neg_hi:[0,1]
	v_pk_add_f32 v[80:81], v[54:55], v[34:35]
	v_pk_add_f32 v[34:35], v[54:55], v[34:35] neg_lo:[0,1] neg_hi:[0,1]
	v_pk_add_f32 v[92:93], v[84:85], v[80:81]
	v_xor_b32_e32 v55, 0x80000000, v34
	v_mov_b32_e32 v54, v35
	v_pk_add_f32 v[80:81], v[84:85], v[80:81] neg_lo:[0,1] neg_hi:[0,1]
	v_pk_add_f32 v[84:85], v[58:59], v[54:55]
	v_pk_add_f32 v[34:35], v[58:59], v[54:55] neg_lo:[0,1] neg_hi:[0,1]
	v_xor_b32_e32 v54, 0x80000000, v95
	v_mov_b32_e32 v55, v95
	v_pk_fma_f32 v[58:59], v[14:15], s[90:91], v[14:15] op_sel:[1,0,0] op_sel_hi:[0,1,1]
	v_pk_mul_f32 v[54:55], v[54:55], s[14:15]
	v_pk_mul_f32 v[88:89], v[58:59], v[88:89] op_sel:[1,0] op_sel_hi:[0,1]
	v_pk_fma_f32 v[54:55], v[94:95], s[94:95], v[54:55] op_sel_hi:[0,1,1]
	v_pk_fma_f32 v[86:87], v[58:59], v[86:87], v[88:89] op_sel_hi:[1,0,1]
	ds_write2_b64 v74, v[54:55], v[86:87] offset1:16
	v_xor_b32_e32 v54, 0x80000000, v59
	v_mov_b32_e32 v55, v59
	v_pk_mul_f32 v[54:55], v[14:15], v[54:55] op_sel:[1,0] op_sel_hi:[0,1]
	v_pk_fma_f32 v[54:55], v[14:15], v[58:59], v[54:55] op_sel_hi:[1,0,1]
	v_xor_b32_e32 v58, 0x80000000, v103
	v_mov_b32_e32 v59, v103
	v_xor_b32_e32 v74, 0x80000000, v55
	v_mov_b32_e32 v75, v55
	v_pk_mul_f32 v[58:59], v[54:55], v[58:59] op_sel:[1,0] op_sel_hi:[0,1]
	v_pk_mul_f32 v[74:75], v[14:15], v[74:75] op_sel:[1,0] op_sel_hi:[0,1]
	v_pk_fma_f32 v[58:59], v[54:55], v[102:103], v[58:59] op_sel_hi:[1,0,1]
	v_pk_fma_f32 v[54:55], v[14:15], v[54:55], v[74:75] op_sel_hi:[1,0,1]
	v_xor_b32_e32 v74, 0x80000000, v57
	v_mov_b32_e32 v75, v57
	v_pk_mul_f32 v[74:75], v[54:55], v[74:75] op_sel:[1,0] op_sel_hi:[0,1]
	v_pk_fma_f32 v[56:57], v[54:55], v[56:57], v[74:75] op_sel_hi:[1,0,1]
	ds_write2_b64 v73, v[58:59], v[56:57] offset0:32 offset1:48
	v_xor_b32_e32 v56, 0x80000000, v55
	v_mov_b32_e32 v57, v55
	v_pk_mul_f32 v[56:57], v[14:15], v[56:57] op_sel:[1,0] op_sel_hi:[0,1]
	v_pk_fma_f32 v[54:55], v[14:15], v[54:55], v[56:57] op_sel_hi:[1,0,1]
	v_xor_b32_e32 v56, 0x80000000, v105
	v_mov_b32_e32 v57, v105
	v_xor_b32_e32 v58, 0x80000000, v55
	v_mov_b32_e32 v59, v55
	v_pk_mul_f32 v[56:57], v[54:55], v[56:57] op_sel:[1,0] op_sel_hi:[0,1]
	v_pk_mul_f32 v[58:59], v[14:15], v[58:59] op_sel:[1,0] op_sel_hi:[0,1]
	v_pk_fma_f32 v[56:57], v[54:55], v[104:105], v[56:57] op_sel_hi:[1,0,1]
	v_pk_fma_f32 v[54:55], v[14:15], v[54:55], v[58:59] op_sel_hi:[1,0,1]
	v_xor_b32_e32 v58, 0x80000000, v83
	v_mov_b32_e32 v59, v83
	v_pk_mul_f32 v[58:59], v[54:55], v[58:59] op_sel:[1,0] op_sel_hi:[0,1]
	v_pk_fma_f32 v[58:59], v[54:55], v[82:83], v[58:59] op_sel_hi:[1,0,1]
	ds_write2_b64 v72, v[56:57], v[58:59] offset0:64 offset1:80
	v_xor_b32_e32 v56, 0x80000000, v55
	v_mov_b32_e32 v57, v55
	v_pk_mul_f32 v[56:57], v[14:15], v[56:57] op_sel:[1,0] op_sel_hi:[0,1]
	v_pk_fma_f32 v[54:55], v[14:15], v[54:55], v[56:57] op_sel_hi:[1,0,1]
	v_xor_b32_e32 v56, 0x80000000, v99
	v_mov_b32_e32 v57, v99
	v_xor_b32_e32 v58, 0x80000000, v55
	v_mov_b32_e32 v59, v55
	v_pk_mul_f32 v[56:57], v[54:55], v[56:57] op_sel:[1,0] op_sel_hi:[0,1]
	v_pk_mul_f32 v[58:59], v[14:15], v[58:59] op_sel:[1,0] op_sel_hi:[0,1]
	v_pk_fma_f32 v[56:57], v[54:55], v[98:99], v[56:57] op_sel_hi:[1,0,1]
	v_pk_fma_f32 v[54:55], v[14:15], v[54:55], v[58:59] op_sel_hi:[1,0,1]
	v_xor_b32_e32 v58, 0x80000000, v93
	v_mov_b32_e32 v59, v93
	v_pk_mul_f32 v[58:59], v[54:55], v[58:59] op_sel:[1,0] op_sel_hi:[0,1]
	v_pk_fma_f32 v[58:59], v[54:55], v[92:93], v[58:59] op_sel_hi:[1,0,1]
	ds_write2_b64 v71, v[56:57], v[58:59] offset0:96 offset1:112
	v_xor_b32_e32 v56, 0x80000000, v55
	v_mov_b32_e32 v57, v55
	v_pk_mul_f32 v[56:57], v[14:15], v[56:57] op_sel:[1,0] op_sel_hi:[0,1]
	v_pk_fma_f32 v[54:55], v[14:15], v[54:55], v[56:57] op_sel_hi:[1,0,1]
	v_xor_b32_e32 v56, 0x80000000, v45
	v_mov_b32_e32 v57, v45
	v_pk_mul_f32 v[56:57], v[54:55], v[56:57] op_sel:[1,0] op_sel_hi:[0,1]
	v_pk_fma_f32 v[44:45], v[54:55], v[44:45], v[56:57] op_sel_hi:[1,0,1]
	v_xor_b32_e32 v56, 0x80000000, v55
	v_mov_b32_e32 v57, v55
	v_pk_mul_f32 v[56:57], v[14:15], v[56:57] op_sel:[1,0] op_sel_hi:[0,1]
	v_pk_fma_f32 v[54:55], v[14:15], v[54:55], v[56:57] op_sel_hi:[1,0,1]
	v_xor_b32_e32 v56, 0x80000000, v91
	v_mov_b32_e32 v57, v91
	v_pk_mul_f32 v[56:57], v[54:55], v[56:57] op_sel:[1,0] op_sel_hi:[0,1]
	v_pk_fma_f32 v[56:57], v[54:55], v[90:91], v[56:57] op_sel_hi:[1,0,1]
	ds_write2_b64 v70, v[44:45], v[56:57] offset0:128 offset1:144
	v_xor_b32_e32 v44, 0x80000000, v55
	v_mov_b32_e32 v45, v55
	v_pk_mul_f32 v[44:45], v[14:15], v[44:45] op_sel:[1,0] op_sel_hi:[0,1]
	v_pk_fma_f32 v[44:45], v[14:15], v[54:55], v[44:45] op_sel_hi:[1,0,1]
	v_xor_b32_e32 v54, 0x80000000, v49
	v_mov_b32_e32 v55, v49
	v_pk_mul_f32 v[54:55], v[44:45], v[54:55] op_sel:[1,0] op_sel_hi:[0,1]
	v_pk_fma_f32 v[48:49], v[44:45], v[48:49], v[54:55] op_sel_hi:[1,0,1]
	v_xor_b32_e32 v54, 0x80000000, v45
	v_mov_b32_e32 v55, v45
	v_pk_mul_f32 v[54:55], v[14:15], v[54:55] op_sel:[1,0] op_sel_hi:[0,1]
	v_pk_fma_f32 v[44:45], v[14:15], v[44:45], v[54:55] op_sel_hi:[1,0,1]
	v_xor_b32_e32 v54, 0x80000000, v53
	v_mov_b32_e32 v55, v53
	v_pk_mul_f32 v[54:55], v[44:45], v[54:55] op_sel:[1,0] op_sel_hi:[0,1]
	v_pk_fma_f32 v[52:53], v[44:45], v[52:53], v[54:55] op_sel_hi:[1,0,1]
	ds_write2_b64 v69, v[48:49], v[52:53] offset0:160 offset1:176
	v_xor_b32_e32 v48, 0x80000000, v45
	v_mov_b32_e32 v49, v45
	v_pk_mul_f32 v[48:49], v[14:15], v[48:49] op_sel:[1,0] op_sel_hi:[0,1]
	v_pk_fma_f32 v[44:45], v[14:15], v[44:45], v[48:49] op_sel_hi:[1,0,1]
	v_xor_b32_e32 v48, 0x80000000, v37
	v_mov_b32_e32 v49, v37
	v_pk_mul_f32 v[48:49], v[48:49], v[44:45] op_sel:[0,1] op_sel_hi:[1,0]
	s_nop 0
	v_pk_fma_f32 v[36:37], v[36:37], v[44:45], v[48:49] op_sel_hi:[0,1,1]
	v_xor_b32_e32 v48, 0x80000000, v45
	v_mov_b32_e32 v49, v45
	v_pk_mul_f32 v[48:49], v[14:15], v[48:49] op_sel:[1,0] op_sel_hi:[0,1]
	v_pk_fma_f32 v[44:45], v[14:15], v[44:45], v[48:49] op_sel_hi:[1,0,1]
	v_xor_b32_e32 v48, 0x80000000, v77
	v_mov_b32_e32 v49, v77
	v_pk_mul_f32 v[48:49], v[44:45], v[48:49] op_sel:[1,0] op_sel_hi:[0,1]
	v_pk_fma_f32 v[48:49], v[44:45], v[76:77], v[48:49] op_sel_hi:[1,0,1]
	ds_write2_b64 v68, v[36:37], v[48:49] offset0:192 offset1:208
	v_xor_b32_e32 v36, 0x80000000, v45
	v_mov_b32_e32 v37, v45
	v_pk_mul_f32 v[36:37], v[14:15], v[36:37] op_sel:[1,0] op_sel_hi:[0,1]
	v_pk_fma_f32 v[36:37], v[14:15], v[44:45], v[36:37] op_sel_hi:[1,0,1]
	v_xor_b32_e32 v44, 0x80000000, v41
	v_mov_b32_e32 v45, v41
	v_pk_mul_f32 v[44:45], v[44:45], v[36:37] op_sel:[0,1] op_sel_hi:[1,0]
	s_nop 0
	v_pk_fma_f32 v[40:41], v[40:41], v[36:37], v[44:45] op_sel_hi:[0,1,1]
	v_xor_b32_e32 v44, 0x80000000, v37
	v_mov_b32_e32 v45, v37
	v_pk_mul_f32 v[44:45], v[14:15], v[44:45] op_sel:[1,0] op_sel_hi:[0,1]
	v_pk_fma_f32 v[36:37], v[14:15], v[36:37], v[44:45] op_sel_hi:[1,0,1]
	v_xor_b32_e32 v44, 0x80000000, v85
	v_mov_b32_e32 v45, v85
	v_pk_mul_f32 v[44:45], v[36:37], v[44:45] op_sel:[1,0] op_sel_hi:[0,1]
	v_pk_fma_f32 v[44:45], v[36:37], v[84:85], v[44:45] op_sel_hi:[1,0,1]
	ds_write2_b64 v67, v[40:41], v[44:45] offset0:224 offset1:240
	v_xor_b32_e32 v40, 0x80000000, v37
	v_mov_b32_e32 v41, v37
	v_pk_mul_f32 v[40:41], v[14:15], v[40:41] op_sel:[1,0] op_sel_hi:[0,1]
	v_pk_fma_f32 v[36:37], v[14:15], v[36:37], v[40:41] op_sel_hi:[1,0,1]
	v_xor_b32_e32 v40, 0x80000000, v29
	v_mov_b32_e32 v41, v29
	v_pk_mul_f32 v[40:41], v[40:41], v[36:37] op_sel:[0,1] op_sel_hi:[1,0]
	s_nop 0
	v_pk_fma_f32 v[28:29], v[28:29], v[36:37], v[40:41] op_sel_hi:[0,1,1]
	v_xor_b32_e32 v40, 0x80000000, v37
	v_mov_b32_e32 v41, v37
	v_pk_mul_f32 v[40:41], v[14:15], v[40:41] op_sel:[1,0] op_sel_hi:[0,1]
	v_pk_fma_f32 v[36:37], v[14:15], v[36:37], v[40:41] op_sel_hi:[1,0,1]
	v_xor_b32_e32 v40, 0x80000000, v79
	v_mov_b32_e32 v41, v79
	v_pk_mul_f32 v[40:41], v[40:41], v[36:37] op_sel:[0,1] op_sel_hi:[1,0]
	s_nop 0
	v_pk_fma_f32 v[40:41], v[78:79], v[36:37], v[40:41] op_sel_hi:[0,1,1]
	ds_write2_b64 v66, v[28:29], v[40:41] offset1:16
	v_xor_b32_e32 v28, 0x80000000, v37
	v_mov_b32_e32 v29, v37
	v_pk_mul_f32 v[28:29], v[14:15], v[28:29] op_sel:[1,0] op_sel_hi:[0,1]
	v_pk_fma_f32 v[28:29], v[14:15], v[36:37], v[28:29] op_sel_hi:[1,0,1]
	v_xor_b32_e32 v36, 0x80000000, v33
	v_mov_b32_e32 v37, v33
	v_pk_mul_f32 v[36:37], v[36:37], v[28:29] op_sel:[0,1] op_sel_hi:[1,0]
	s_nop 0
	v_pk_fma_f32 v[32:33], v[32:33], v[28:29], v[36:37] op_sel_hi:[0,1,1]
	v_xor_b32_e32 v36, 0x80000000, v29
	v_mov_b32_e32 v37, v29
	v_pk_mul_f32 v[36:37], v[14:15], v[36:37] op_sel:[1,0] op_sel_hi:[0,1]
	v_pk_fma_f32 v[28:29], v[14:15], v[28:29], v[36:37] op_sel_hi:[1,0,1]
	v_xor_b32_e32 v36, 0x80000000, v51
	v_mov_b32_e32 v37, v51
	v_pk_mul_f32 v[36:37], v[36:37], v[28:29] op_sel:[0,1] op_sel_hi:[1,0]
	s_nop 0
	v_pk_fma_f32 v[36:37], v[50:51], v[28:29], v[36:37] op_sel_hi:[0,1,1]
	ds_write2_b64 v65, v[32:33], v[36:37] offset0:32 offset1:48
	v_xor_b32_e32 v32, 0x80000000, v29
	v_mov_b32_e32 v33, v29
	v_pk_mul_f32 v[32:33], v[14:15], v[32:33] op_sel:[1,0] op_sel_hi:[0,1]
	v_pk_fma_f32 v[28:29], v[14:15], v[28:29], v[32:33] op_sel_hi:[1,0,1]
	v_xor_b32_e32 v32, 0x80000000, v25
	v_mov_b32_e32 v33, v25
	v_pk_mul_f32 v[32:33], v[32:33], v[28:29] op_sel:[0,1] op_sel_hi:[1,0]
	s_nop 0
	v_pk_fma_f32 v[24:25], v[24:25], v[28:29], v[32:33] op_sel_hi:[0,1,1]
	v_xor_b32_e32 v32, 0x80000000, v29
	v_mov_b32_e32 v33, v29
	v_pk_mul_f32 v[32:33], v[14:15], v[32:33] op_sel:[1,0] op_sel_hi:[0,1]
	v_pk_fma_f32 v[28:29], v[14:15], v[28:29], v[32:33] op_sel_hi:[1,0,1]
	v_xor_b32_e32 v32, 0x80000000, v47
	v_mov_b32_e32 v33, v47
	v_pk_mul_f32 v[32:33], v[32:33], v[28:29] op_sel:[0,1] op_sel_hi:[1,0]
	s_nop 0
	v_pk_fma_f32 v[32:33], v[46:47], v[28:29], v[32:33] op_sel_hi:[0,1,1]
	ds_write2_b64 v64, v[24:25], v[32:33] offset0:64 offset1:80
	v_xor_b32_e32 v24, 0x80000000, v29
	v_mov_b32_e32 v25, v29
	v_pk_mul_f32 v[24:25], v[14:15], v[24:25] op_sel:[1,0] op_sel_hi:[0,1]
	v_pk_fma_f32 v[24:25], v[14:15], v[28:29], v[24:25] op_sel_hi:[1,0,1]
	v_xor_b32_e32 v28, 0x80000000, v27
	v_mov_b32_e32 v29, v27
	v_pk_mul_f32 v[28:29], v[28:29], v[24:25] op_sel:[0,1] op_sel_hi:[1,0]
	s_nop 0
	v_pk_fma_f32 v[26:27], v[26:27], v[24:25], v[28:29] op_sel_hi:[0,1,1]
	v_xor_b32_e32 v28, 0x80000000, v25
	v_mov_b32_e32 v29, v25
	v_pk_mul_f32 v[28:29], v[14:15], v[28:29] op_sel:[1,0] op_sel_hi:[0,1]
	v_pk_fma_f32 v[24:25], v[14:15], v[24:25], v[28:29] op_sel_hi:[1,0,1]
	v_xor_b32_e32 v28, 0x80000000, v81
	v_mov_b32_e32 v29, v81
	v_pk_mul_f32 v[28:29], v[28:29], v[24:25] op_sel:[0,1] op_sel_hi:[1,0]
	s_nop 0
	v_pk_fma_f32 v[28:29], v[80:81], v[24:25], v[28:29] op_sel_hi:[0,1,1]
	ds_write2_b64 v63, v[26:27], v[28:29] offset0:96 offset1:112
	v_xor_b32_e32 v26, 0x80000000, v25
	v_mov_b32_e32 v27, v25
	v_pk_mul_f32 v[26:27], v[14:15], v[26:27] op_sel:[1,0] op_sel_hi:[0,1]
	v_pk_fma_f32 v[24:25], v[14:15], v[24:25], v[26:27] op_sel_hi:[1,0,1]
	v_xor_b32_e32 v26, 0x80000000, v21
	v_mov_b32_e32 v27, v21
	v_pk_mul_f32 v[26:27], v[26:27], v[24:25] op_sel:[0,1] op_sel_hi:[1,0]
	s_nop 0
	v_pk_fma_f32 v[20:21], v[20:21], v[24:25], v[26:27] op_sel_hi:[0,1,1]
	v_xor_b32_e32 v26, 0x80000000, v25
	v_mov_b32_e32 v27, v25
	v_pk_mul_f32 v[26:27], v[14:15], v[26:27] op_sel:[1,0] op_sel_hi:[0,1]
	v_pk_fma_f32 v[24:25], v[14:15], v[24:25], v[26:27] op_sel_hi:[1,0,1]
	v_xor_b32_e32 v26, 0x80000000, v39
	v_mov_b32_e32 v27, v39
	v_pk_mul_f32 v[26:27], v[26:27], v[24:25] op_sel:[0,1] op_sel_hi:[1,0]
	s_nop 0
	v_pk_fma_f32 v[26:27], v[38:39], v[24:25], v[26:27] op_sel_hi:[0,1,1]
	ds_write2_b64 v62, v[20:21], v[26:27] offset0:128 offset1:144
	v_xor_b32_e32 v20, 0x80000000, v25
	v_mov_b32_e32 v21, v25
	v_pk_mul_f32 v[20:21], v[14:15], v[20:21] op_sel:[1,0] op_sel_hi:[0,1]
	v_pk_fma_f32 v[20:21], v[14:15], v[24:25], v[20:21] op_sel_hi:[1,0,1]
	v_xor_b32_e32 v24, 0x80000000, v23
	v_mov_b32_e32 v25, v23
	v_pk_mul_f32 v[24:25], v[24:25], v[20:21] op_sel:[0,1] op_sel_hi:[1,0]
	s_nop 0
	v_pk_fma_f32 v[22:23], v[22:23], v[20:21], v[24:25] op_sel_hi:[0,1,1]
	v_xor_b32_e32 v24, 0x80000000, v21
	v_mov_b32_e32 v25, v21
	v_pk_mul_f32 v[24:25], v[14:15], v[24:25] op_sel:[1,0] op_sel_hi:[0,1]
	v_pk_fma_f32 v[20:21], v[14:15], v[20:21], v[24:25] op_sel_hi:[1,0,1]
	v_xor_b32_e32 v24, 0x80000000, v43
	v_mov_b32_e32 v25, v43
	v_pk_mul_f32 v[24:25], v[24:25], v[20:21] op_sel:[0,1] op_sel_hi:[1,0]
	s_nop 0
	v_pk_fma_f32 v[24:25], v[42:43], v[20:21], v[24:25] op_sel_hi:[0,1,1]
	ds_write2_b64 v61, v[22:23], v[24:25] offset0:160 offset1:176
	v_xor_b32_e32 v22, 0x80000000, v21
	v_mov_b32_e32 v23, v21
	v_pk_mul_f32 v[22:23], v[14:15], v[22:23] op_sel:[1,0] op_sel_hi:[0,1]
	v_pk_fma_f32 v[20:21], v[14:15], v[20:21], v[22:23] op_sel_hi:[1,0,1]
	v_xor_b32_e32 v22, 0x80000000, v17
	v_mov_b32_e32 v23, v17
	v_pk_mul_f32 v[22:23], v[22:23], v[20:21] op_sel:[0,1] op_sel_hi:[1,0]
	s_nop 0
	v_pk_fma_f32 v[16:17], v[16:17], v[20:21], v[22:23] op_sel_hi:[0,1,1]
	v_xor_b32_e32 v22, 0x80000000, v21
	v_mov_b32_e32 v23, v21
	v_pk_mul_f32 v[22:23], v[14:15], v[22:23] op_sel:[1,0] op_sel_hi:[0,1]
	v_pk_fma_f32 v[20:21], v[14:15], v[20:21], v[22:23] op_sel_hi:[1,0,1]
	v_xor_b32_e32 v22, 0x80000000, v31
	v_mov_b32_e32 v23, v31
	v_pk_mul_f32 v[22:23], v[22:23], v[20:21] op_sel:[0,1] op_sel_hi:[1,0]
	s_nop 0
	v_pk_fma_f32 v[22:23], v[30:31], v[20:21], v[22:23] op_sel_hi:[0,1,1]
	ds_write2_b64 v60, v[16:17], v[22:23] offset0:192 offset1:208
	v_xor_b32_e32 v16, 0x80000000, v21
	v_mov_b32_e32 v17, v21
	v_pk_mul_f32 v[16:17], v[14:15], v[16:17] op_sel:[1,0] op_sel_hi:[0,1]
	v_pk_fma_f32 v[16:17], v[14:15], v[20:21], v[16:17] op_sel_hi:[1,0,1]
	v_xor_b32_e32 v20, 0x80000000, v19
	v_mov_b32_e32 v21, v19
	v_pk_mul_f32 v[20:21], v[20:21], v[16:17] op_sel:[0,1] op_sel_hi:[1,0]
	s_nop 0
	v_pk_fma_f32 v[18:19], v[18:19], v[16:17], v[20:21] op_sel_hi:[0,1,1]
	v_xor_b32_e32 v20, 0x80000000, v17
	v_mov_b32_e32 v21, v17
	v_pk_mul_f32 v[20:21], v[14:15], v[20:21] op_sel:[1,0] op_sel_hi:[0,1]
	v_pk_fma_f32 v[14:15], v[14:15], v[16:17], v[20:21] op_sel_hi:[1,0,1]
	v_xor_b32_e32 v16, 0x80000000, v35
	v_mov_b32_e32 v17, v35
	v_pk_mul_f32 v[16:17], v[16:17], v[14:15] op_sel:[0,1] op_sel_hi:[1,0]
	s_nop 0
	v_pk_fma_f32 v[14:15], v[34:35], v[14:15], v[16:17] op_sel_hi:[0,1,1]
	ds_write2_b64 v13, v[18:19], v[14:15] offset0:224 offset1:240
	v_mov_b32_e32 v14, v182
	v_mov_b32_e32 v10, v176
	v_mov_b32_e32 v13, v175
	s_waitcnt lgkmcnt(0)
	s_barrier
	v_mov_b32_e32 v48, v167
	v_xor_b32_e32 v16, 1, v13
	v_lshlrev_b32_e32 v10, 3, v10
	v_lshlrev_b32_e32 v16, 3, v16
	v_add3_u32 v18, 0, v16, v10
	v_xor_b32_e32 v16, 2, v13
	v_lshlrev_b32_e32 v16, 3, v16
	v_xor_b32_e32 v24, 5, v13
	v_add3_u32 v20, 0, v16, v10
	v_xor_b32_e32 v16, 3, v13
	v_lshlrev_b32_e32 v24, 3, v24
	v_lshlrev_b32_e32 v15, 3, v13
	v_lshlrev_b32_e32 v16, 3, v16
	v_add3_u32 v26, 0, v24, v10
	v_xor_b32_e32 v24, 6, v13
	v_add3_u32 v15, 0, v15, v10
	v_add3_u32 v22, 0, v16, v10
	v_lshlrev_b32_e32 v24, 3, v24
	v_xor_b32_e32 v32, 9, v13
	ds_read_b64 v[16:17], v15
	ds_read_b64 v[18:19], v18
	ds_read_b64 v[20:21], v20
	ds_read_b64 v[22:23], v22
	v_xor_b32_e32 v15, 4, v13
	v_add3_u32 v28, 0, v24, v10
	v_xor_b32_e32 v24, 7, v13
	v_lshlrev_b32_e32 v32, 3, v32
	v_lshlrev_b32_e32 v15, 3, v15
	v_lshlrev_b32_e32 v24, 3, v24
	v_add3_u32 v34, 0, v32, v10
	v_xor_b32_e32 v32, 10, v13
	v_add3_u32 v15, 0, v15, v10
	v_add3_u32 v30, 0, v24, v10
	v_lshlrev_b32_e32 v32, 3, v32
	ds_read_b64 v[24:25], v15
	ds_read_b64 v[26:27], v26
	ds_read_b64 v[28:29], v28
	ds_read_b64 v[30:31], v30
	v_xor_b32_e32 v15, 8, v13
	v_add3_u32 v36, 0, v32, v10
	v_xor_b32_e32 v32, 11, v13
	v_lshlrev_b32_e32 v15, 3, v15
	v_lshlrev_b32_e32 v32, 3, v32
	v_xor_b32_e32 v40, 13, v13
	v_add3_u32 v15, 0, v15, v10
	v_add3_u32 v38, 0, v32, v10
	v_lshlrev_b32_e32 v40, 3, v40
	ds_read_b64 v[32:33], v15
	ds_read_b64 v[34:35], v34
	ds_read_b64 v[36:37], v36
	ds_read_b64 v[38:39], v38
	v_xor_b32_e32 v15, 12, v13
	v_add3_u32 v42, 0, v40, v10
	v_xor_b32_e32 v40, 14, v13
	v_xor_b32_e32 v13, 15, v13
	v_lshlrev_b32_e32 v15, 3, v15
	v_lshlrev_b32_e32 v40, 3, v40
	v_lshlrev_b32_e32 v13, 3, v13
	v_add3_u32 v15, 0, v15, v10
	v_add3_u32 v44, 0, v40, v10
	v_add3_u32 v10, 0, v13, v10
	ds_read_b64 v[40:41], v15
	ds_read_b64 v[42:43], v42
	ds_read_b64 v[44:45], v44
	ds_read_b64 v[46:47], v10
	v_mov_b32_e32 v10, v1
	v_mov_b32_e32 v13, v166
	v_mov_b32_e32 v10, v164
	s_waitcnt lgkmcnt(7)
	v_pk_add_f32 v[52:53], v[16:17], v[32:33]
	v_mov_b32_e32 v10, v165
	v_pk_add_f32 v[16:17], v[16:17], v[32:33] neg_lo:[0,1] neg_hi:[0,1]
	s_waitcnt lgkmcnt(6)
	v_pk_add_f32 v[32:33], v[18:19], v[34:35]
	v_pk_add_f32 v[18:19], v[18:19], v[34:35] neg_lo:[0,1] neg_hi:[0,1]
	v_mov_b32_e32 v13, v168
	v_mov_b32_e32 v50, v169
	v_xor_b32_e32 v34, 0x80000000, v19
	v_mov_b32_e32 v35, v18
	v_ashrrev_i32_e32 v15, 31, v14
	v_pk_mul_f32 v[34:35], v[34:35], v[50:51] op_sel_hi:[1,0] neg_lo:[0,1] neg_hi:[0,1]
	v_mov_b32_e32 v13, v170
	v_pk_fma_f32 v[18:19], v[18:19], v[10:11], v[34:35] op_sel_hi:[1,0,1]
	s_waitcnt lgkmcnt(5)
	v_pk_add_f32 v[34:35], v[20:21], v[36:37]
	v_pk_add_f32 v[20:21], v[20:21], v[36:37] neg_lo:[0,1] neg_hi:[0,1]
	s_nop 0
	v_xor_b32_e32 v36, 0x80000000, v21
	v_mov_b32_e32 v37, v20
	v_pk_mul_f32 v[36:37], v[36:37], v[48:49] op_sel_hi:[1,0] neg_lo:[0,1] neg_hi:[0,1]
	v_mov_b32_e32 v13, v171
	v_pk_fma_f32 v[20:21], v[20:21], v[48:49], v[36:37] op_sel_hi:[1,0,1]
	s_waitcnt lgkmcnt(4)
	v_pk_add_f32 v[36:37], v[22:23], v[38:39]
	v_pk_add_f32 v[22:23], v[22:23], v[38:39] neg_lo:[0,1] neg_hi:[0,1]
	s_nop 0
	v_pk_mul_f32 v[38:39], v[22:23], v[50:51] op_sel_hi:[1,0]
	v_xor_b32_e32 v54, 0x80000000, v23
	v_mov_b32_e32 v55, v22
	v_pk_fma_f32 v[22:23], v[54:55], v[10:11], v[38:39] op_sel_hi:[1,0,1] neg_lo:[0,1,0] neg_hi:[0,1,0]
	s_waitcnt lgkmcnt(3)
	v_pk_add_f32 v[38:39], v[24:25], v[40:41]
	v_pk_add_f32 v[24:25], v[24:25], v[40:41] neg_lo:[0,1] neg_hi:[0,1]
	v_mov_b32_e32 v13, v175
	v_xor_b32_e32 v41, 0x80000000, v24
	v_mov_b32_e32 v40, v25
	s_waitcnt lgkmcnt(2)
	v_pk_add_f32 v[24:25], v[26:27], v[42:43]
	v_pk_add_f32 v[26:27], v[26:27], v[42:43] neg_lo:[0,1] neg_hi:[0,1]
	s_nop 0
	v_pk_mul_f32 v[42:43], v[26:27], v[50:51] op_sel_hi:[1,0] neg_lo:[0,1] neg_hi:[0,1]
	v_xor_b32_e32 v54, 0x80000000, v27
	v_mov_b32_e32 v55, v26
	v_pk_fma_f32 v[26:27], v[54:55], v[10:11], v[42:43] op_sel_hi:[1,0,1] neg_lo:[0,1,0] neg_hi:[0,1,0]
	s_waitcnt lgkmcnt(1)
	v_pk_add_f32 v[42:43], v[28:29], v[44:45]
	v_pk_add_f32 v[28:29], v[28:29], v[44:45] neg_lo:[0,1] neg_hi:[0,1]
	s_nop 0
	v_xor_b32_e32 v44, 0x80000000, v29
	v_mov_b32_e32 v45, v28
	v_pk_mul_f32 v[44:45], v[44:45], v[48:49] op_sel_hi:[1,0] neg_lo:[0,1] neg_hi:[0,1]
	s_nop 0
	v_pk_fma_f32 v[28:29], v[28:29], v[48:49], v[44:45] op_sel_hi:[1,0,1] neg_lo:[0,1,0] neg_hi:[0,1,0]
	s_waitcnt lgkmcnt(0)
	v_pk_add_f32 v[44:45], v[30:31], v[46:47]
	v_pk_add_f32 v[30:31], v[30:31], v[46:47] neg_lo:[0,1] neg_hi:[0,1]
	s_nop 0
	v_xor_b32_e32 v46, 0x80000000, v31
	v_mov_b32_e32 v47, v30
	v_pk_mul_f32 v[46:47], v[46:47], v[50:51] op_sel_hi:[1,0] neg_lo:[0,1] neg_hi:[0,1]
	v_pk_add_f32 v[50:51], v[32:33], v[24:25]
	v_pk_add_f32 v[24:25], v[32:33], v[24:25] neg_lo:[0,1] neg_hi:[0,1]
	v_pk_fma_f32 v[30:31], v[30:31], v[10:11], v[46:47] op_sel_hi:[1,0,1] neg_lo:[0,1,0] neg_hi:[0,1,0]
	v_xor_b32_e32 v32, 0x80000000, v25
	v_mov_b32_e32 v33, v24
	v_pk_mul_f32 v[32:33], v[32:33], v[48:49] op_sel_hi:[1,0] neg_lo:[0,1] neg_hi:[0,1]
	v_pk_add_f32 v[46:47], v[52:53], v[38:39]
	v_pk_fma_f32 v[24:25], v[24:25], v[48:49], v[32:33] op_sel_hi:[1,0,1]
	v_pk_add_f32 v[32:33], v[34:35], v[42:43]
	v_pk_add_f32 v[34:35], v[34:35], v[42:43] neg_lo:[0,1] neg_hi:[0,1]
	v_pk_add_f32 v[38:39], v[52:53], v[38:39] neg_lo:[0,1] neg_hi:[0,1]
	v_xor_b32_e32 v43, 0x80000000, v34
	v_mov_b32_e32 v42, v35
	v_pk_add_f32 v[34:35], v[36:37], v[44:45]
	v_pk_add_f32 v[36:37], v[36:37], v[44:45] neg_lo:[0,1] neg_hi:[0,1]
	v_mov_b32_e32 v10, v177
	v_xor_b32_e32 v44, 0x80000000, v37
	v_mov_b32_e32 v45, v36
	v_pk_mul_f32 v[44:45], v[44:45], v[48:49] op_sel_hi:[1,0] neg_lo:[0,1] neg_hi:[0,1]
	s_nop 0
	v_pk_fma_f32 v[36:37], v[36:37], v[48:49], v[44:45] op_sel_hi:[1,0,1] neg_lo:[0,1,0] neg_hi:[0,1,0]
	v_pk_add_f32 v[44:45], v[46:47], v[32:33]
	v_pk_add_f32 v[32:33], v[46:47], v[32:33] neg_lo:[0,1] neg_hi:[0,1]
	v_pk_add_f32 v[46:47], v[50:51], v[34:35]
	v_pk_add_f32 v[34:35], v[50:51], v[34:35] neg_lo:[0,1] neg_hi:[0,1]
	s_nop 0
	v_xor_b32_e32 v51, 0x80000000, v34
	v_mov_b32_e32 v50, v35
	v_pk_add_f32 v[34:35], v[44:45], v[46:47]
	v_pk_add_f32 v[44:45], v[44:45], v[46:47] neg_lo:[0,1] neg_hi:[0,1]
	v_pk_add_f32 v[46:47], v[32:33], v[50:51]
	v_pk_add_f32 v[32:33], v[32:33], v[50:51] neg_lo:[0,1] neg_hi:[0,1]
	v_pk_add_f32 v[50:51], v[38:39], v[42:43]
	v_pk_add_f32 v[38:39], v[38:39], v[42:43] neg_lo:[0,1] neg_hi:[0,1]
	v_pk_add_f32 v[42:43], v[24:25], v[36:37]
	v_pk_add_f32 v[24:25], v[24:25], v[36:37] neg_lo:[0,1] neg_hi:[0,1]
	s_nop 0
	v_xor_b32_e32 v37, 0x80000000, v24
	v_mov_b32_e32 v36, v25
	v_pk_add_f32 v[24:25], v[50:51], v[42:43]
	v_pk_add_f32 v[42:43], v[50:51], v[42:43] neg_lo:[0,1] neg_hi:[0,1]
	v_pk_add_f32 v[50:51], v[38:39], v[36:37]
	v_pk_add_f32 v[36:37], v[38:39], v[36:37] neg_lo:[0,1] neg_hi:[0,1]
	v_pk_add_f32 v[38:39], v[16:17], v[40:41]
	v_pk_add_f32 v[16:17], v[16:17], v[40:41] neg_lo:[0,1] neg_hi:[0,1]
	v_pk_add_f32 v[40:41], v[18:19], v[26:27]
	v_pk_add_f32 v[18:19], v[18:19], v[26:27] neg_lo:[0,1] neg_hi:[0,1]
	s_nop 0
	v_xor_b32_e32 v26, 0x80000000, v19
	v_mov_b32_e32 v27, v18
	v_pk_mul_f32 v[26:27], v[48:49], v[26:27] op_sel_hi:[0,1] neg_lo:[1,0] neg_hi:[1,0]
	v_pk_fma_f32 v[18:19], v[48:49], v[18:19], v[26:27] op_sel_hi:[0,1,1]
	v_pk_add_f32 v[26:27], v[20:21], v[28:29]
	v_pk_add_f32 v[20:21], v[20:21], v[28:29] neg_lo:[0,1] neg_hi:[0,1]
	s_nop 0
	v_xor_b32_e32 v29, 0x80000000, v20
	v_mov_b32_e32 v28, v21
	v_pk_add_f32 v[20:21], v[22:23], v[30:31]
	v_pk_add_f32 v[22:23], v[22:23], v[30:31] neg_lo:[0,1] neg_hi:[0,1]
	s_nop 0
	v_xor_b32_e32 v30, 0x80000000, v23
	v_mov_b32_e32 v31, v22
	v_pk_mul_f32 v[30:31], v[48:49], v[30:31] op_sel_hi:[0,1] neg_lo:[1,0] neg_hi:[1,0]
	v_pk_fma_f32 v[22:23], v[48:49], v[22:23], v[30:31] op_sel_hi:[0,1,1] neg_lo:[1,0,0] neg_hi:[1,0,0]
	v_pk_add_f32 v[30:31], v[38:39], v[26:27]
	v_pk_add_f32 v[26:27], v[38:39], v[26:27] neg_lo:[0,1] neg_hi:[0,1]
	v_pk_add_f32 v[38:39], v[40:41], v[20:21]
	v_pk_add_f32 v[20:21], v[40:41], v[20:21] neg_lo:[0,1] neg_hi:[0,1]
	v_mov_b32_e32 v48, v167
	v_xor_b32_e32 v41, 0x80000000, v20
	v_mov_b32_e32 v40, v21
	v_pk_add_f32 v[20:21], v[30:31], v[38:39]
	v_pk_add_f32 v[30:31], v[30:31], v[38:39] neg_lo:[0,1] neg_hi:[0,1]
	v_pk_add_f32 v[38:39], v[26:27], v[40:41]
	v_pk_add_f32 v[26:27], v[26:27], v[40:41] neg_lo:[0,1] neg_hi:[0,1]
	v_pk_add_f32 v[40:41], v[16:17], v[28:29]
	v_pk_add_f32 v[16:17], v[16:17], v[28:29] neg_lo:[0,1] neg_hi:[0,1]
	v_pk_add_f32 v[28:29], v[18:19], v[22:23]
	v_pk_add_f32 v[18:19], v[18:19], v[22:23] neg_lo:[0,1] neg_hi:[0,1]
	s_nop 0
	v_xor_b32_e32 v23, 0x80000000, v18
	v_mov_b32_e32 v22, v19
	v_pk_add_f32 v[18:19], v[40:41], v[28:29]
	v_pk_add_f32 v[28:29], v[40:41], v[28:29] neg_lo:[0,1] neg_hi:[0,1]
	v_pk_add_f32 v[40:41], v[16:17], v[22:23]
	v_pk_add_f32 v[16:17], v[16:17], v[22:23] neg_lo:[0,1] neg_hi:[0,1]
	v_lshl_add_u64 v[22:23], v[14:15], 3, s[46:47]
	global_store_dwordx2 v[22:23], v[34:35], off
	v_add_u32_e32 v22, 0x200, v14
	v_ashrrev_i32_e32 v23, 31, v22
	v_lshl_add_u64 v[22:23], v[22:23], 3, s[46:47]
	global_store_dwordx2 v[22:23], v[20:21], off
	v_add_u32_e32 v20, 0x400, v14
	v_ashrrev_i32_e32 v21, 31, v20
	v_lshl_add_u64 v[20:21], v[20:21], 3, s[46:47]
	global_store_dwordx2 v[20:21], v[24:25], off
	v_add_u32_e32 v20, 0x600, v14
	v_ashrrev_i32_e32 v21, 31, v20
	v_lshl_add_u64 v[20:21], v[20:21], 3, s[46:47]
	global_store_dwordx2 v[20:21], v[18:19], off
	v_add_u32_e32 v18, 0x800, v14
	v_ashrrev_i32_e32 v19, 31, v18
	v_lshl_add_u64 v[18:19], v[18:19], 3, s[46:47]
	global_store_dwordx2 v[18:19], v[46:47], off
	v_add_u32_e32 v18, 0xa00, v14
	v_ashrrev_i32_e32 v19, 31, v18
	v_lshl_add_u64 v[18:19], v[18:19], 3, s[46:47]
	global_store_dwordx2 v[18:19], v[38:39], off
	v_add_u32_e32 v18, 0xc00, v14
	v_ashrrev_i32_e32 v19, 31, v18
	v_lshl_add_u64 v[18:19], v[18:19], 3, s[46:47]
	global_store_dwordx2 v[18:19], v[50:51], off
	v_add_u32_e32 v18, 0xe00, v14
	v_ashrrev_i32_e32 v19, 31, v18
	v_lshl_add_u64 v[18:19], v[18:19], 3, s[46:47]
	global_store_dwordx2 v[18:19], v[40:41], off
	v_add_u32_e32 v18, 0x1000, v14
	v_ashrrev_i32_e32 v19, 31, v18
	v_lshl_add_u64 v[18:19], v[18:19], 3, s[46:47]
	global_store_dwordx2 v[18:19], v[44:45], off
	v_add_u32_e32 v18, 0x1200, v14
	v_ashrrev_i32_e32 v19, 31, v18
	v_lshl_add_u64 v[18:19], v[18:19], 3, s[46:47]
	global_store_dwordx2 v[18:19], v[30:31], off
	v_add_u32_e32 v18, 0x1400, v14
	v_ashrrev_i32_e32 v19, 31, v18
	v_lshl_add_u64 v[18:19], v[18:19], 3, s[46:47]
	global_store_dwordx2 v[18:19], v[42:43], off
	v_add_u32_e32 v18, 0x1600, v14
	v_ashrrev_i32_e32 v19, 31, v18
	v_lshl_add_u64 v[18:19], v[18:19], 3, s[46:47]
	global_store_dwordx2 v[18:19], v[28:29], off
	v_add_u32_e32 v18, 0x1800, v14
	v_ashrrev_i32_e32 v19, 31, v18
	v_lshl_add_u64 v[18:19], v[18:19], 3, s[46:47]
	global_store_dwordx2 v[18:19], v[32:33], off
	v_add_u32_e32 v18, 0x1a00, v14
	v_ashrrev_i32_e32 v19, 31, v18
	v_lshl_add_u64 v[18:19], v[18:19], 3, s[46:47]
	global_store_dwordx2 v[18:19], v[26:27], off
	v_add_u32_e32 v18, 0x1c00, v14
	v_ashrrev_i32_e32 v19, 31, v18
	v_lshl_add_u64 v[18:19], v[18:19], 3, s[46:47]
	global_store_dwordx2 v[18:19], v[36:37], off
	v_add_u32_e32 v18, 0x1e00, v14
	v_ashrrev_i32_e32 v19, 31, v18
	v_lshl_add_u64 v[18:19], v[18:19], 3, s[46:47]
	global_store_dwordx2 v[18:19], v[16:17], off
	v_mov_b32_e32 v50, v169
	v_xor_b32_e32 v16, 1, v13
	v_lshlrev_b32_e32 v10, 3, v10
	v_lshlrev_b32_e32 v16, 3, v16
	v_add3_u32 v18, 0, v16, v10
	v_xor_b32_e32 v16, 2, v13
	v_lshlrev_b32_e32 v16, 3, v16
	v_xor_b32_e32 v24, 5, v13
	v_add3_u32 v20, 0, v16, v10
	v_xor_b32_e32 v16, 3, v13
	v_lshlrev_b32_e32 v24, 3, v24
	v_lshlrev_b32_e32 v15, 3, v13
	v_lshlrev_b32_e32 v16, 3, v16
	v_add3_u32 v26, 0, v24, v10
	v_xor_b32_e32 v24, 6, v13
	v_add3_u32 v15, 0, v15, v10
	v_add3_u32 v22, 0, v16, v10
	v_lshlrev_b32_e32 v24, 3, v24
	v_xor_b32_e32 v32, 9, v13
	ds_read_b64 v[16:17], v15
	ds_read_b64 v[18:19], v18
	ds_read_b64 v[20:21], v20
	ds_read_b64 v[22:23], v22
	v_xor_b32_e32 v15, 4, v13
	v_add3_u32 v28, 0, v24, v10
	v_xor_b32_e32 v24, 7, v13
	v_lshlrev_b32_e32 v32, 3, v32
	v_lshlrev_b32_e32 v15, 3, v15
	v_lshlrev_b32_e32 v24, 3, v24
	v_add3_u32 v34, 0, v32, v10
	v_xor_b32_e32 v32, 10, v13
	v_add3_u32 v15, 0, v15, v10
	v_add3_u32 v30, 0, v24, v10
	v_lshlrev_b32_e32 v32, 3, v32
	ds_read_b64 v[24:25], v15
	ds_read_b64 v[26:27], v26
	ds_read_b64 v[28:29], v28
	ds_read_b64 v[30:31], v30
	v_xor_b32_e32 v15, 8, v13
	v_add3_u32 v36, 0, v32, v10
	v_xor_b32_e32 v32, 11, v13
	v_lshlrev_b32_e32 v15, 3, v15
	v_lshlrev_b32_e32 v32, 3, v32
	v_xor_b32_e32 v40, 13, v13
	v_add3_u32 v15, 0, v15, v10
	v_add3_u32 v38, 0, v32, v10
	v_lshlrev_b32_e32 v40, 3, v40
	ds_read_b64 v[32:33], v15
	ds_read_b64 v[34:35], v34
	ds_read_b64 v[36:37], v36
	ds_read_b64 v[38:39], v38
	v_xor_b32_e32 v15, 12, v13
	v_add3_u32 v42, 0, v40, v10
	v_xor_b32_e32 v40, 14, v13
	v_xor_b32_e32 v13, 15, v13
	v_lshlrev_b32_e32 v15, 3, v15
	v_lshlrev_b32_e32 v40, 3, v40
	v_lshlrev_b32_e32 v13, 3, v13
	v_add3_u32 v15, 0, v15, v10
	v_add3_u32 v44, 0, v40, v10
	v_add3_u32 v10, 0, v13, v10
	ds_read_b64 v[40:41], v15
	ds_read_b64 v[42:43], v42
	ds_read_b64 v[44:45], v44
	ds_read_b64 v[46:47], v10
	v_mov_b32_e32 v10, v1
	v_mov_b32_e32 v13, v166
	v_mov_b32_e32 v10, v164
	s_waitcnt lgkmcnt(7)
	v_pk_add_f32 v[52:53], v[16:17], v[32:33]
	v_mov_b32_e32 v10, v165
	v_pk_add_f32 v[16:17], v[16:17], v[32:33] neg_lo:[0,1] neg_hi:[0,1]
	s_waitcnt lgkmcnt(6)
	v_pk_add_f32 v[32:33], v[18:19], v[34:35]
	v_pk_add_f32 v[18:19], v[18:19], v[34:35] neg_lo:[0,1] neg_hi:[0,1]
	v_mov_b32_e32 v13, v168
	v_xor_b32_e32 v34, 0x80000000, v19
	v_mov_b32_e32 v35, v18
	s_nop 0
	v_pk_mul_f32 v[34:35], v[34:35], v[50:51] op_sel_hi:[1,0] neg_lo:[0,1] neg_hi:[0,1]
	v_mov_b32_e32 v13, v170
	v_pk_fma_f32 v[18:19], v[18:19], v[10:11], v[34:35] op_sel_hi:[1,0,1]
	s_waitcnt lgkmcnt(5)
	v_pk_add_f32 v[34:35], v[20:21], v[36:37]
	v_pk_add_f32 v[20:21], v[20:21], v[36:37] neg_lo:[0,1] neg_hi:[0,1]
	s_nop 0
	v_xor_b32_e32 v36, 0x80000000, v21
	v_mov_b32_e32 v37, v20
	v_pk_mul_f32 v[36:37], v[36:37], v[48:49] op_sel_hi:[1,0] neg_lo:[0,1] neg_hi:[0,1]
	v_mov_b32_e32 v13, v171
	v_pk_fma_f32 v[20:21], v[20:21], v[48:49], v[36:37] op_sel_hi:[1,0,1]
	s_waitcnt lgkmcnt(4)
	v_pk_add_f32 v[36:37], v[22:23], v[38:39]
	v_pk_add_f32 v[22:23], v[22:23], v[38:39] neg_lo:[0,1] neg_hi:[0,1]
	s_nop 0
	v_pk_mul_f32 v[38:39], v[22:23], v[50:51] op_sel_hi:[1,0]
	v_xor_b32_e32 v54, 0x80000000, v23
	v_mov_b32_e32 v55, v22
	v_pk_fma_f32 v[22:23], v[54:55], v[10:11], v[38:39] op_sel_hi:[1,0,1] neg_lo:[0,1,0] neg_hi:[0,1,0]
	s_waitcnt lgkmcnt(3)
	v_pk_add_f32 v[38:39], v[24:25], v[40:41]
	v_pk_add_f32 v[24:25], v[24:25], v[40:41] neg_lo:[0,1] neg_hi:[0,1]
	v_mov_b32_e32 v13, v173
	v_xor_b32_e32 v41, 0x80000000, v24
	v_mov_b32_e32 v40, v25
	s_waitcnt lgkmcnt(2)
	v_pk_add_f32 v[24:25], v[26:27], v[42:43]
	v_pk_add_f32 v[26:27], v[26:27], v[42:43] neg_lo:[0,1] neg_hi:[0,1]
	s_nop 0
	v_pk_mul_f32 v[42:43], v[26:27], v[50:51] op_sel_hi:[1,0] neg_lo:[0,1] neg_hi:[0,1]
	v_xor_b32_e32 v54, 0x80000000, v27
	v_mov_b32_e32 v55, v26
	v_pk_fma_f32 v[26:27], v[54:55], v[10:11], v[42:43] op_sel_hi:[1,0,1] neg_lo:[0,1,0] neg_hi:[0,1,0]
	s_waitcnt lgkmcnt(1)
	v_pk_add_f32 v[42:43], v[28:29], v[44:45]
	v_pk_add_f32 v[28:29], v[28:29], v[44:45] neg_lo:[0,1] neg_hi:[0,1]
	s_nop 0
	v_xor_b32_e32 v44, 0x80000000, v29
	v_mov_b32_e32 v45, v28
	v_pk_mul_f32 v[44:45], v[44:45], v[48:49] op_sel_hi:[1,0] neg_lo:[0,1] neg_hi:[0,1]
	s_nop 0
	v_pk_fma_f32 v[28:29], v[28:29], v[48:49], v[44:45] op_sel_hi:[1,0,1] neg_lo:[0,1,0] neg_hi:[0,1,0]
	s_waitcnt lgkmcnt(0)
	v_pk_add_f32 v[44:45], v[30:31], v[46:47]
	v_pk_add_f32 v[30:31], v[30:31], v[46:47] neg_lo:[0,1] neg_hi:[0,1]
	s_nop 0
	v_xor_b32_e32 v46, 0x80000000, v31
	v_mov_b32_e32 v47, v30
	v_pk_mul_f32 v[46:47], v[46:47], v[50:51] op_sel_hi:[1,0] neg_lo:[0,1] neg_hi:[0,1]
	v_pk_add_f32 v[50:51], v[32:33], v[24:25]
	v_pk_add_f32 v[24:25], v[32:33], v[24:25] neg_lo:[0,1] neg_hi:[0,1]
	v_pk_fma_f32 v[30:31], v[30:31], v[10:11], v[46:47] op_sel_hi:[1,0,1] neg_lo:[0,1,0] neg_hi:[0,1,0]
	v_xor_b32_e32 v32, 0x80000000, v25
	v_mov_b32_e32 v33, v24
	v_pk_mul_f32 v[32:33], v[32:33], v[48:49] op_sel_hi:[1,0] neg_lo:[0,1] neg_hi:[0,1]
	v_pk_add_f32 v[46:47], v[52:53], v[38:39]
	v_pk_fma_f32 v[24:25], v[24:25], v[48:49], v[32:33] op_sel_hi:[1,0,1]
	v_pk_add_f32 v[32:33], v[34:35], v[42:43]
	v_pk_add_f32 v[34:35], v[34:35], v[42:43] neg_lo:[0,1] neg_hi:[0,1]
	v_pk_add_f32 v[38:39], v[52:53], v[38:39] neg_lo:[0,1] neg_hi:[0,1]
	v_xor_b32_e32 v43, 0x80000000, v34
	v_mov_b32_e32 v42, v35
	v_pk_add_f32 v[34:35], v[36:37], v[44:45]
	v_pk_add_f32 v[36:37], v[36:37], v[44:45] neg_lo:[0,1] neg_hi:[0,1]
	v_mov_b32_e32 v10, v183
	v_xor_b32_e32 v44, 0x80000000, v37
	v_mov_b32_e32 v45, v36
	v_pk_mul_f32 v[44:45], v[44:45], v[48:49] op_sel_hi:[1,0] neg_lo:[0,1] neg_hi:[0,1]
	s_nop 0
	v_pk_fma_f32 v[36:37], v[36:37], v[48:49], v[44:45] op_sel_hi:[1,0,1] neg_lo:[0,1,0] neg_hi:[0,1,0]
	v_pk_add_f32 v[44:45], v[46:47], v[32:33]
	v_pk_add_f32 v[32:33], v[46:47], v[32:33] neg_lo:[0,1] neg_hi:[0,1]
	v_pk_add_f32 v[46:47], v[50:51], v[34:35]
	v_pk_add_f32 v[34:35], v[50:51], v[34:35] neg_lo:[0,1] neg_hi:[0,1]
	s_nop 0
	v_xor_b32_e32 v51, 0x80000000, v34
	v_mov_b32_e32 v50, v35
	v_pk_add_f32 v[34:35], v[44:45], v[46:47]
	v_pk_add_f32 v[44:45], v[44:45], v[46:47] neg_lo:[0,1] neg_hi:[0,1]
	v_pk_add_f32 v[46:47], v[32:33], v[50:51]
	v_pk_add_f32 v[32:33], v[32:33], v[50:51] neg_lo:[0,1] neg_hi:[0,1]
	v_pk_add_f32 v[50:51], v[38:39], v[42:43]
	v_pk_add_f32 v[38:39], v[38:39], v[42:43] neg_lo:[0,1] neg_hi:[0,1]
	v_pk_add_f32 v[42:43], v[24:25], v[36:37]
	v_pk_add_f32 v[24:25], v[24:25], v[36:37] neg_lo:[0,1] neg_hi:[0,1]
	s_nop 0
	v_xor_b32_e32 v37, 0x80000000, v24
	v_mov_b32_e32 v36, v25
	v_pk_add_f32 v[24:25], v[50:51], v[42:43]
	v_pk_add_f32 v[42:43], v[50:51], v[42:43] neg_lo:[0,1] neg_hi:[0,1]
	v_pk_add_f32 v[50:51], v[38:39], v[36:37]
	v_pk_add_f32 v[36:37], v[38:39], v[36:37] neg_lo:[0,1] neg_hi:[0,1]
	v_pk_add_f32 v[38:39], v[16:17], v[40:41]
	v_pk_add_f32 v[16:17], v[16:17], v[40:41] neg_lo:[0,1] neg_hi:[0,1]
	v_pk_add_f32 v[40:41], v[18:19], v[26:27]
	v_pk_add_f32 v[18:19], v[18:19], v[26:27] neg_lo:[0,1] neg_hi:[0,1]
	s_nop 0
	v_xor_b32_e32 v26, 0x80000000, v19
	v_mov_b32_e32 v27, v18
	v_pk_mul_f32 v[26:27], v[48:49], v[26:27] op_sel_hi:[0,1] neg_lo:[1,0] neg_hi:[1,0]
	v_pk_fma_f32 v[18:19], v[48:49], v[18:19], v[26:27] op_sel_hi:[0,1,1]
	v_pk_add_f32 v[26:27], v[20:21], v[28:29]
	v_pk_add_f32 v[20:21], v[20:21], v[28:29] neg_lo:[0,1] neg_hi:[0,1]
	s_nop 0
	v_xor_b32_e32 v29, 0x80000000, v20
	v_mov_b32_e32 v28, v21
	v_pk_add_f32 v[20:21], v[22:23], v[30:31]
	v_pk_add_f32 v[22:23], v[22:23], v[30:31] neg_lo:[0,1] neg_hi:[0,1]
	s_nop 0
	v_xor_b32_e32 v30, 0x80000000, v23
	v_mov_b32_e32 v31, v22
	v_pk_mul_f32 v[30:31], v[48:49], v[30:31] op_sel_hi:[0,1] neg_lo:[1,0] neg_hi:[1,0]
	v_pk_fma_f32 v[22:23], v[48:49], v[22:23], v[30:31] op_sel_hi:[0,1,1] neg_lo:[1,0,0] neg_hi:[1,0,0]
	v_pk_add_f32 v[30:31], v[38:39], v[26:27]
	v_pk_add_f32 v[26:27], v[38:39], v[26:27] neg_lo:[0,1] neg_hi:[0,1]
	v_pk_add_f32 v[38:39], v[40:41], v[20:21]
	v_pk_add_f32 v[20:21], v[40:41], v[20:21] neg_lo:[0,1] neg_hi:[0,1]
	s_nop 0
	v_xor_b32_e32 v41, 0x80000000, v20
	v_mov_b32_e32 v40, v21
	v_pk_add_f32 v[20:21], v[30:31], v[38:39]
	v_pk_add_f32 v[30:31], v[30:31], v[38:39] neg_lo:[0,1] neg_hi:[0,1]
	v_pk_add_f32 v[38:39], v[26:27], v[40:41]
	v_pk_add_f32 v[26:27], v[26:27], v[40:41] neg_lo:[0,1] neg_hi:[0,1]
	v_pk_add_f32 v[40:41], v[16:17], v[28:29]
	v_pk_add_f32 v[16:17], v[16:17], v[28:29] neg_lo:[0,1] neg_hi:[0,1]
	v_pk_add_f32 v[28:29], v[18:19], v[22:23]
	v_pk_add_f32 v[18:19], v[18:19], v[22:23] neg_lo:[0,1] neg_hi:[0,1]
	s_nop 0
	v_xor_b32_e32 v23, 0x80000000, v18
	v_mov_b32_e32 v22, v19
	v_pk_add_f32 v[18:19], v[40:41], v[28:29]
	v_pk_add_f32 v[28:29], v[40:41], v[28:29] neg_lo:[0,1] neg_hi:[0,1]
	v_pk_add_f32 v[40:41], v[16:17], v[22:23]
	v_pk_add_f32 v[16:17], v[16:17], v[22:23] neg_lo:[0,1] neg_hi:[0,1]
	v_add_u32_e32 v22, 0x2000, v14
	v_ashrrev_i32_e32 v23, 31, v22
	v_lshl_add_u64 v[22:23], v[22:23], 3, s[46:47]
	global_store_dwordx2 v[22:23], v[34:35], off
	v_add_u32_e32 v22, 0x2200, v14
	v_ashrrev_i32_e32 v23, 31, v22
	v_lshl_add_u64 v[22:23], v[22:23], 3, s[46:47]
	global_store_dwordx2 v[22:23], v[20:21], off
	v_add_u32_e32 v20, 0x2400, v14
	v_ashrrev_i32_e32 v21, 31, v20
	v_lshl_add_u64 v[20:21], v[20:21], 3, s[46:47]
	global_store_dwordx2 v[20:21], v[24:25], off
	v_add_u32_e32 v20, 0x2600, v14
	v_ashrrev_i32_e32 v21, 31, v20
	v_lshl_add_u64 v[20:21], v[20:21], 3, s[46:47]
	global_store_dwordx2 v[20:21], v[18:19], off
	v_add_u32_e32 v18, 0x2800, v14
	v_ashrrev_i32_e32 v19, 31, v18
	v_lshl_add_u64 v[18:19], v[18:19], 3, s[46:47]
	global_store_dwordx2 v[18:19], v[46:47], off
	v_add_u32_e32 v18, 0x2a00, v14
	v_ashrrev_i32_e32 v19, 31, v18
	v_lshl_add_u64 v[18:19], v[18:19], 3, s[46:47]
	global_store_dwordx2 v[18:19], v[38:39], off
	v_add_u32_e32 v18, 0x2c00, v14
	v_ashrrev_i32_e32 v19, 31, v18
	v_lshl_add_u64 v[18:19], v[18:19], 3, s[46:47]
	global_store_dwordx2 v[18:19], v[50:51], off
	v_add_u32_e32 v18, 0x2e00, v14
	v_ashrrev_i32_e32 v19, 31, v18
	v_lshl_add_u64 v[18:19], v[18:19], 3, s[46:47]
	global_store_dwordx2 v[18:19], v[40:41], off
	v_add_u32_e32 v18, 0x3000, v14
	v_ashrrev_i32_e32 v19, 31, v18
	v_lshl_add_u64 v[18:19], v[18:19], 3, s[46:47]
	global_store_dwordx2 v[18:19], v[44:45], off
	v_add_u32_e32 v18, 0x3200, v14
	v_ashrrev_i32_e32 v19, 31, v18
	v_lshl_add_u64 v[18:19], v[18:19], 3, s[46:47]
	global_store_dwordx2 v[18:19], v[30:31], off
	v_add_u32_e32 v18, 0x3400, v14
	v_ashrrev_i32_e32 v19, 31, v18
	v_lshl_add_u64 v[18:19], v[18:19], 3, s[46:47]
	global_store_dwordx2 v[18:19], v[42:43], off
	v_add_u32_e32 v18, 0x3600, v14
	v_ashrrev_i32_e32 v19, 31, v18
	v_lshl_add_u64 v[18:19], v[18:19], 3, s[46:47]
	global_store_dwordx2 v[18:19], v[28:29], off
	v_add_u32_e32 v18, 0x3800, v14
	v_ashrrev_i32_e32 v19, 31, v18
	v_lshl_add_u64 v[18:19], v[18:19], 3, s[46:47]
	global_store_dwordx2 v[18:19], v[32:33], off
	v_add_u32_e32 v18, 0x3a00, v14
	v_ashrrev_i32_e32 v19, 31, v18
	v_lshl_add_u64 v[18:19], v[18:19], 3, s[46:47]
	global_store_dwordx2 v[18:19], v[26:27], off
	v_add_u32_e32 v18, 0x3c00, v14
	v_add_u32_e32 v14, 0x3e00, v14
	v_ashrrev_i32_e32 v15, 31, v14
	v_ashrrev_i32_e32 v19, 31, v18
	v_lshl_add_u64 v[14:15], v[14:15], 3, s[46:47]
	v_lshl_add_u64 v[18:19], v[18:19], 3, s[46:47]
	global_store_dwordx2 v[14:15], v[16:17], off
	v_mov_b32_e32 v16, v184
	v_mov_b32_e32 v14, v182
	global_store_dwordx2 v[18:19], v[36:37], off
	s_barrier
	s_nop 0
	v_pk_mul_f32 v[36:37], v[16:17], s[64:65] op_sel_hi:[0,1] neg_lo:[1,0]
	s_mov_b64 s[64:65], vcc
	v_ashrrev_i32_e32 v15, 31, v14
	v_lshl_add_u64 v[18:19], v[14:15], 2, s[64:65]
	s_movk_i32 vcc_lo, 0x1000
	v_add_co_u32_e32 v28, vcc, vcc_lo, v18
	v_pk_mul_f32 v[40:41], v[16:17], s[78:79] op_sel_hi:[0,1] neg_lo:[1,0]
	s_nop 0
	v_addc_co_u32_e32 v29, vcc, 0, v19, vcc
	v_add_co_u32_e32 v20, vcc, s39, v18
	s_movk_i32 s78, 0x3000
	s_nop 0
	v_addc_co_u32_e32 v21, vcc, 0, v19, vcc
	v_add_co_u32_e32 v48, vcc, s78, v18
	v_pk_mul_f32 v[32:33], v[16:17], s[40:41] op_sel_hi:[0,1] neg_lo:[1,0]
	s_nop 0
	v_addc_co_u32_e32 v49, vcc, 0, v19, vcc
	v_add_co_u32_e32 v22, vcc, s72, v18
	s_mov_b32 s40, 0x3f7ec46d
	s_nop 0
	v_addc_co_u32_e32 v23, vcc, 0, v19, vcc
	v_add_co_u32_e32 v58, vcc, s33, v18
	s_mov_b32 s33, 0x8000
	s_nop 0
	v_addc_co_u32_e32 v59, vcc, 0, v19, vcc
	v_add_co_u32_e32 v60, vcc, s43, v18
	s_mov_b32 s41, 0xbdc8bd36
	s_nop 0
	v_addc_co_u32_e32 v61, vcc, 0, v19, vcc
	v_add_co_u32_e32 v64, vcc, s73, v18
	v_pk_mul_f32 v[34:35], v[16:17], s[76:77] op_sel_hi:[0,1] neg_lo:[1,0]
	s_nop 0
	v_addc_co_u32_e32 v65, vcc, 0, v19, vcc
	v_add_co_u32_e32 v68, vcc, s33, v18
	s_mov_b32 s33, 0x9000
	s_nop 0
	v_addc_co_u32_e32 v69, vcc, 0, v19, vcc
	v_add_co_u32_e32 v24, vcc, s33, v18
	s_mov_b32 s33, 0xa000
	s_nop 0
	v_addc_co_u32_e32 v25, vcc, 0, v19, vcc
	v_add_co_u32_e32 v26, vcc, s33, v18
	s_mov_b32 s33, 0xb000
	s_nop 0
	v_addc_co_u32_e32 v27, vcc, 0, v19, vcc
	v_add_co_u32_e32 v30, vcc, s33, v18
	s_mov_b32 s33, 0xc000
	s_nop 0
	v_addc_co_u32_e32 v31, vcc, 0, v19, vcc
	v_add_co_u32_e32 v38, vcc, s33, v18
	s_mov_b32 s33, 0xd000
	s_nop 0
	v_addc_co_u32_e32 v39, vcc, 0, v19, vcc
	v_add_co_u32_e32 v44, vcc, s33, v18
	s_mov_b32 s33, 0xe000
	s_nop 0
	v_addc_co_u32_e32 v45, vcc, 0, v19, vcc
	v_add_co_u32_e32 v50, vcc, s33, v18
	s_mov_b32 s33, 0xf000
	s_nop 0
	v_addc_co_u32_e32 v51, vcc, 0, v19, vcc
	v_add_co_u32_e32 v70, vcc, s33, v18
	v_pk_mul_f32 v[92:93], v[16:17], s[62:63] op_sel_hi:[0,1] neg_lo:[1,0]
	s_nop 0
	v_addc_co_u32_e32 v71, vcc, 0, v19, vcc
	global_load_dword v94, v[68:69], off
	global_load_dword v96, v[68:69], off offset:2048
	global_load_dword v98, v[26:27], off offset:-4096
	global_load_dword v100, v[24:25], off offset:2048
	global_load_dword v102, v[26:27], off
	global_load_dword v104, v[26:27], off offset:2048
	global_load_dword v106, v[38:39], off offset:-4096
	global_load_dword v108, v[30:31], off offset:2048
	global_load_dword v110, v[38:39], off
	global_load_dword v112, v[38:39], off offset:2048
	global_load_dword v114, v[50:51], off offset:-4096
	global_load_dword v116, v[44:45], off offset:2048
	global_load_dword v118, v[50:51], off
	global_load_dword v120, v[50:51], off offset:2048
	global_load_dword v122, v[70:71], off
	global_load_dword v56, v[20:21], off
	s_nop 0
	global_load_dword v50, v[20:21], off offset:2048
	global_load_dword v124, v[70:71], off offset:2048
	global_load_dword v44, v[22:23], off offset:-4096
	global_load_dword v38, v[22:23], off
	global_load_dword v72, v[20:21], off offset:-4096
	global_load_dword v30, v[22:23], off offset:2048
	global_load_dword v26, v[60:61], off offset:-4096
	global_load_dword v24, v[60:61], off
	s_nop 0
	global_load_dword v22, v[60:61], off offset:2048
	global_load_dword v20, v[68:69], off offset:-4096
	global_load_dword v74, v[18:19], off
	global_load_dword v78, v[18:19], off offset:2048
	s_nop 0
	global_load_dword v68, v[28:29], off offset:2048
	s_nop 0
	global_load_dword v48, v[48:49], off offset:2048
	s_nop 0
	global_load_dword v28, v[58:59], off offset:2048
	global_load_dword v18, v[64:65], off offset:2048
	v_pk_mul_f32 v[52:53], v[16:17], s[58:59] op_sel_hi:[0,1] neg_lo:[1,0]
	v_pk_fma_f32 v[82:83], v[10:11], s[40:41], v[34:35] op_sel_hi:[0,1,1]
	v_pk_fma_f32 v[34:35], v[10:11], s[92:93], v[92:93] op_sel_hi:[0,1,1]
	s_mov_b32 s92, 0x3e47c5c2
	v_pk_mul_f32 v[66:67], v[16:17], s[60:61] op_sel_hi:[0,1] neg_lo:[1,0]
	v_pk_fma_f32 v[84:85], v[10:11], s[44:45], v[32:33] op_sel_hi:[0,1,1]
	v_pk_fma_f32 v[60:61], v[10:11], s[82:83], v[52:53] op_sel_hi:[0,1,1]
	s_mov_b32 s82, 0x3f45e403
	s_mov_b32 s93, 0xbf7b14be
	v_pk_mul_f32 v[32:33], v[16:17], s[30:31] op_sel_hi:[0,1] neg_lo:[1,0]
	s_mov_b32 s30, 0x3dc8bd36
	v_pk_mul_f32 v[54:55], v[16:17], s[74:75] op_sel_hi:[0,1] neg_lo:[1,0]
	v_pk_mul_f32 v[62:63], v[16:17], s[54:55] op_sel_hi:[0,1] neg_lo:[1,0]
	s_mov_b32 s83, 0xbf226799
	v_pk_fma_f32 v[52:53], v[10:11], s[86:87], v[66:67] op_sel_hi:[0,1,1]
	s_mov_b32 s31, 0xbf7ec46d
	v_pk_fma_f32 v[66:67], v[10:11], s[92:93], v[32:33] op_sel_hi:[0,1,1]
	v_pk_mul_f32 v[32:33], v[16:17], s[34:35] op_sel_hi:[0,1] neg_lo:[1,0]
	v_pk_fma_f32 v[76:77], v[10:11], s[80:81], v[40:41] op_sel_hi:[0,1,1]
	s_mov_b32 s80, 0x3f61c598
	v_pk_fma_f32 v[58:59], v[10:11], s[82:83], v[54:55] op_sel_hi:[0,1,1]
	v_pk_fma_f32 v[54:55], v[10:11], s[84:85], v[62:63] op_sel_hi:[0,1,1]
	s_mov_b32 s86, 0x3f0e39da
	v_pk_fma_f32 v[62:63], v[10:11], s[30:31], v[32:33] op_sel_hi:[0,1,1]
	v_pk_mul_f32 v[32:33], v[16:17], s[36:37] op_sel_hi:[0,1] neg_lo:[1,0]
	v_pk_mul_f32 v[46:47], v[16:17], s[48:49] op_sel_hi:[0,1] neg_lo:[1,0]
	v_pk_mul_f32 v[86:87], v[16:17], s[66:67] op_sel_hi:[0,1] neg_lo:[1,0]
	s_mov_b32 s81, 0xbef15aea
	s_mov_b32 s87, 0xbf54db31
	v_pk_fma_f32 v[32:33], v[10:11], s[96:97], v[32:33] op_sel_hi:[0,1,1]
	s_mov_b32 s54, 0x3f6c835e
	v_pk_fma_f32 v[64:65], v[10:11], s[80:81], v[46:47] op_sel_hi:[0,1,1]
	v_pk_fma_f32 v[46:47], v[10:11], s[86:87], v[86:87] op_sel_hi:[0,1,1]
	v_pk_mul_f32 v[42:43], v[16:17], s[50:51] op_sel_hi:[0,1] neg_lo:[1,0]
	v_pk_mul_f32 v[88:89], v[16:17], s[68:69] op_sel_hi:[0,1] neg_lo:[1,0]
	s_mov_b32 s55, 0xbec3ef15
	v_pk_fma_f32 v[70:71], v[10:11], s[54:55], v[42:43] op_sel_hi:[0,1,1]
	v_pk_fma_f32 v[42:43], v[10:11], s[88:89], v[88:89] op_sel_hi:[0,1,1]
	s_mov_b32 s88, 0x3ec3ef15
	v_pk_mul_f32 v[90:91], v[16:17], s[56:57] op_sel_hi:[0,1] neg_lo:[1,0]
	s_mov_b32 s89, 0xbf6c835e
	v_pk_fma_f32 v[40:41], v[10:11], s[88:89], v[90:91] op_sel_hi:[0,1,1]
	s_mov_b32 s76, 0x3f7b14be
	s_mov_b32 s77, 0xbe47c5c2
	v_pk_fma_f32 v[80:81], v[10:11], s[76:77], v[36:37] op_sel_hi:[0,1,1]
	v_mov_b32_e32 v36, v169
	v_mov_b32_e32 v15, v171
	s_waitcnt vmcnt(31)
	v_pk_mul_f32 v[86:87], v[32:33], v[94:95] op_sel_hi:[1,0]
	v_pk_mul_f32 v[32:33], v[16:17], s[2:3] op_sel_hi:[0,1] neg_lo:[1,0]
	v_pk_fma_f32 v[32:33], v[10:11], s[0:1], v[32:33] op_sel_hi:[0,1,1]
	s_waitcnt vmcnt(30)
	v_pk_mul_f32 v[88:89], v[32:33], v[96:97] op_sel_hi:[1,0]
	v_pk_mul_f32 v[32:33], v[16:17], s[6:7] op_sel_hi:[0,1] neg_lo:[1,0]
	v_pk_fma_f32 v[32:33], v[10:11], s[4:5], v[32:33] op_sel_hi:[0,1,1]
	s_waitcnt vmcnt(29)
	v_pk_mul_f32 v[90:91], v[32:33], v[98:99] op_sel_hi:[1,0]
	v_pk_mul_f32 v[32:33], v[16:17], s[10:11] op_sel_hi:[0,1] neg_lo:[1,0]
	v_pk_fma_f32 v[32:33], v[10:11], s[8:9], v[32:33] op_sel_hi:[0,1,1]
	s_waitcnt vmcnt(28)
	v_pk_mul_f32 v[92:93], v[32:33], v[100:101] op_sel_hi:[1,0]
	v_pk_mul_f32 v[32:33], v[16:17], s[16:17] op_sel_hi:[0,1] neg_lo:[1,0]
	v_pk_fma_f32 v[32:33], v[10:11], s[12:13], v[32:33] op_sel_hi:[0,1,1]
	s_waitcnt vmcnt(27)
	v_pk_mul_f32 v[94:95], v[32:33], v[102:103] op_sel_hi:[1,0]
	v_pk_mul_f32 v[32:33], v[16:17], s[20:21] op_sel_hi:[0,1] neg_lo:[1,0]
	v_pk_fma_f32 v[32:33], v[10:11], s[18:19], v[32:33] op_sel_hi:[0,1,1]
	s_waitcnt vmcnt(26)
	v_pk_mul_f32 v[96:97], v[32:33], v[104:105] op_sel_hi:[1,0]
	v_pk_mul_f32 v[32:33], v[16:17], s[24:25] op_sel_hi:[0,1] neg_lo:[1,0]
	v_pk_fma_f32 v[32:33], v[10:11], s[22:23], v[32:33] op_sel_hi:[0,1,1]
	s_waitcnt vmcnt(25)
	v_pk_mul_f32 v[98:99], v[32:33], v[106:107] op_sel_hi:[1,0]
	v_pk_mul_f32 v[32:33], v[16:17], s[28:29] op_sel_hi:[0,1] neg_lo:[1,0]
	v_pk_fma_f32 v[32:33], v[10:11], s[26:27], v[32:33] op_sel_hi:[0,1,1]
	s_waitcnt vmcnt(24)
	v_pk_mul_f32 v[100:101], v[32:33], v[108:109] op_sel_hi:[1,0]
	v_pk_mul_f32 v[32:33], v[16:17], s[84:85] op_sel_hi:[0,0] neg_lo:[1,0]
	v_pk_fma_f32 v[32:33], v[10:11], s[38:39], v[32:33] op_sel_hi:[0,0,1] neg_lo:[0,0,1] neg_hi:[0,0,1]
	s_waitcnt vmcnt(23)
	v_pk_mul_f32 v[102:103], v[32:33], v[110:111] op_sel_hi:[1,0]
	v_pk_mul_f32 v[32:33], v[16:17], s[26:27] op_sel_hi:[0,1] neg_lo:[1,0]
	v_pk_fma_f32 v[32:33], v[10:11], s[28:29], v[32:33] op_sel_hi:[0,1,1]
	s_waitcnt vmcnt(22)
	v_pk_mul_f32 v[104:105], v[32:33], v[112:113] op_sel_hi:[1,0]
	v_pk_mul_f32 v[32:33], v[16:17], s[22:23] op_sel_hi:[0,1] neg_lo:[1,0]
	v_pk_fma_f32 v[32:33], v[10:11], s[24:25], v[32:33] op_sel_hi:[0,1,1]
	s_waitcnt vmcnt(21)
	v_pk_mul_f32 v[106:107], v[32:33], v[114:115] op_sel_hi:[1,0]
	v_pk_mul_f32 v[32:33], v[16:17], s[18:19] op_sel_hi:[0,1] neg_lo:[1,0]
	v_pk_fma_f32 v[32:33], v[10:11], s[20:21], v[32:33] op_sel_hi:[0,1,1]
	s_waitcnt vmcnt(20)
	v_pk_mul_f32 v[108:109], v[32:33], v[116:117] op_sel_hi:[1,0]
	v_pk_mul_f32 v[32:33], v[16:17], s[12:13] op_sel_hi:[0,1] neg_lo:[1,0]
	v_pk_fma_f32 v[32:33], v[10:11], s[16:17], v[32:33] op_sel_hi:[0,1,1]
	s_waitcnt vmcnt(19)
	v_pk_mul_f32 v[110:111], v[32:33], v[118:119] op_sel_hi:[1,0]
	v_pk_mul_f32 v[32:33], v[16:17], s[8:9] op_sel_hi:[0,1] neg_lo:[1,0]
	v_pk_fma_f32 v[32:33], v[10:11], s[10:11], v[32:33] op_sel_hi:[0,1,1]
	s_waitcnt vmcnt(18)
	v_pk_mul_f32 v[112:113], v[32:33], v[120:121] op_sel_hi:[1,0]
	v_pk_mul_f32 v[32:33], v[16:17], s[4:5] op_sel_hi:[0,1] neg_lo:[1,0]
	v_pk_mul_f32 v[16:17], v[16:17], s[0:1] op_sel_hi:[0,1] neg_lo:[1,0]
	v_pk_fma_f32 v[16:17], v[10:11], s[2:3], v[16:17] op_sel_hi:[0,1,1]
	v_pk_fma_f32 v[32:33], v[10:11], s[6:7], v[32:33] op_sel_hi:[0,1,1]
	s_waitcnt vmcnt(14)
	v_pk_mul_f32 v[116:117], v[16:17], v[124:125] op_sel_hi:[1,0]
	v_mov_b32_e32 v16, v178
	v_mov_b32_e32 v17, v179
	v_mov_b32_e32 v10, v1
	s_waitcnt vmcnt(5)
	v_pk_fma_f32 v[126:127], v[74:75], v[84:85], v[86:87] op_sel_hi:[0,1,1]
	v_pk_fma_f32 v[74:75], v[74:75], v[84:85], v[86:87] op_sel_hi:[0,1,1] neg_lo:[0,0,1] neg_hi:[0,0,1]
	s_waitcnt vmcnt(4)
	v_pk_fma_f32 v[84:85], v[82:83], v[78:79], v[88:89] op_sel_hi:[1,0,1]
	v_pk_fma_f32 v[78:79], v[82:83], v[78:79], v[88:89] op_sel_hi:[1,0,1] neg_lo:[0,0,1] neg_hi:[0,0,1]
	v_pk_mul_f32 v[114:115], v[32:33], v[122:123] op_sel_hi:[1,0]
	v_mov_b32_e32 v118, v164
	v_mov_b32_e32 v32, v165
	v_mov_b32_e32 v120, v166
	v_mov_b32_e32 v10, v167
	v_mov_b32_e32 v122, v168
	v_mov_b32_e32 v124, v170
	v_xor_b32_e32 v82, 0x80000000, v79
	v_mov_b32_e32 v83, v78
	s_nop 0
	v_pk_mul_f32 v[82:83], v[82:83], v[124:125] op_sel_hi:[1,0] neg_lo:[0,1] neg_hi:[0,1]
	s_nop 0
	v_pk_fma_f32 v[78:79], v[78:79], v[118:119], v[82:83] op_sel_hi:[1,0,1]
	v_pk_fma_f32 v[82:83], v[80:81], v[72:73], v[90:91] op_sel_hi:[1,0,1]
	v_pk_fma_f32 v[72:73], v[80:81], v[72:73], v[90:91] op_sel_hi:[1,0,1] neg_lo:[0,0,1] neg_hi:[0,0,1]
	s_nop 0
	v_xor_b32_e32 v80, 0x80000000, v73
	v_mov_b32_e32 v81, v72
	v_pk_mul_f32 v[80:81], v[80:81], v[36:37] op_sel_hi:[1,0] neg_lo:[0,1] neg_hi:[0,1]
	s_nop 0
	v_pk_fma_f32 v[72:73], v[72:73], v[32:33], v[80:81] op_sel_hi:[1,0,1]
	s_waitcnt vmcnt(3)
	v_pk_fma_f32 v[80:81], v[76:77], v[68:69], v[92:93] op_sel_hi:[1,0,1]
	v_pk_fma_f32 v[68:69], v[76:77], v[68:69], v[92:93] op_sel_hi:[1,0,1] neg_lo:[0,0,1] neg_hi:[0,0,1]
	s_nop 0
	v_xor_b32_e32 v76, 0x80000000, v69
	v_mov_b32_e32 v77, v68
	v_pk_mul_f32 v[76:77], v[76:77], v[122:123] op_sel_hi:[1,0] neg_lo:[0,1] neg_hi:[0,1]
	s_nop 0
	v_pk_fma_f32 v[68:69], v[68:69], v[120:121], v[76:77] op_sel_hi:[1,0,1]
	v_pk_fma_f32 v[76:77], v[70:71], v[56:57], v[94:95] op_sel_hi:[1,0,1]
	v_pk_fma_f32 v[56:57], v[70:71], v[56:57], v[94:95] op_sel_hi:[1,0,1] neg_lo:[0,0,1] neg_hi:[0,0,1]
	s_nop 0
	v_xor_b32_e32 v70, 0x80000000, v57
	v_mov_b32_e32 v71, v56
	v_pk_mul_f32 v[70:71], v[70:71], v[10:11] op_sel_hi:[1,0] neg_lo:[0,1] neg_hi:[0,1]
	s_nop 0
	v_pk_fma_f32 v[56:57], v[56:57], v[10:11], v[70:71] op_sel_hi:[1,0,1]
	v_pk_fma_f32 v[70:71], v[64:65], v[50:51], v[96:97] op_sel_hi:[1,0,1]
	v_pk_fma_f32 v[50:51], v[64:65], v[50:51], v[96:97] op_sel_hi:[1,0,1] neg_lo:[0,0,1] neg_hi:[0,0,1]
	s_nop 0
	v_pk_mul_f32 v[64:65], v[50:51], v[122:123] op_sel_hi:[1,0]
	v_xor_b32_e32 v86, 0x80000000, v51
	v_mov_b32_e32 v87, v50
	v_pk_fma_f32 v[50:51], v[60:61], v[44:45], v[98:99] op_sel_hi:[1,0,1]
	v_pk_fma_f32 v[44:45], v[60:61], v[44:45], v[98:99] op_sel_hi:[1,0,1] neg_lo:[0,0,1] neg_hi:[0,0,1]
	v_pk_fma_f32 v[64:65], v[86:87], v[120:121], v[64:65] op_sel_hi:[1,0,1] neg_lo:[0,1,0] neg_hi:[0,1,0]
	v_pk_mul_f32 v[60:61], v[44:45], v[36:37] op_sel_hi:[1,0]
	v_xor_b32_e32 v86, 0x80000000, v45
	v_mov_b32_e32 v87, v44
	s_waitcnt vmcnt(2)
	v_pk_fma_f32 v[44:45], v[58:59], v[48:49], v[100:101] op_sel_hi:[1,0,1]
	v_pk_fma_f32 v[48:49], v[58:59], v[48:49], v[100:101] op_sel_hi:[1,0,1] neg_lo:[0,0,1] neg_hi:[0,0,1]
	v_pk_fma_f32 v[60:61], v[86:87], v[32:33], v[60:61] op_sel_hi:[1,0,1] neg_lo:[0,1,0] neg_hi:[0,1,0]
	v_pk_mul_f32 v[58:59], v[48:49], v[124:125] op_sel_hi:[1,0]
	v_xor_b32_e32 v86, 0x80000000, v49
	v_mov_b32_e32 v87, v48
	v_pk_fma_f32 v[48:49], v[86:87], v[118:119], v[58:59] op_sel_hi:[1,0,1] neg_lo:[0,1,0] neg_hi:[0,1,0]
	v_pk_fma_f32 v[58:59], v[54:55], v[38:39], v[102:103] op_sel_hi:[1,0,1]
	v_pk_fma_f32 v[38:39], v[54:55], v[38:39], v[102:103] op_sel_hi:[1,0,1] neg_lo:[0,0,1] neg_hi:[0,0,1]
	s_nop 0
	v_xor_b32_e32 v55, 0x80000000, v38
	v_mov_b32_e32 v54, v39
	v_pk_fma_f32 v[38:39], v[52:53], v[30:31], v[104:105] op_sel_hi:[1,0,1]
	v_pk_fma_f32 v[30:31], v[52:53], v[30:31], v[104:105] op_sel_hi:[1,0,1] neg_lo:[0,0,1] neg_hi:[0,0,1]
	s_nop 0
	v_pk_mul_f32 v[52:53], v[30:31], v[124:125] op_sel_hi:[1,0] neg_lo:[0,1] neg_hi:[0,1]
	v_xor_b32_e32 v86, 0x80000000, v31
	v_mov_b32_e32 v87, v30
	v_pk_fma_f32 v[30:31], v[46:47], v[26:27], v[106:107] op_sel_hi:[1,0,1]
	v_pk_fma_f32 v[26:27], v[46:47], v[26:27], v[106:107] op_sel_hi:[1,0,1] neg_lo:[0,0,1] neg_hi:[0,0,1]
	v_pk_fma_f32 v[52:53], v[86:87], v[118:119], v[52:53] op_sel_hi:[1,0,1] neg_lo:[0,1,0] neg_hi:[0,1,0]
	v_pk_mul_f32 v[46:47], v[26:27], v[36:37] op_sel_hi:[1,0] neg_lo:[0,1] neg_hi:[0,1]
	v_xor_b32_e32 v86, 0x80000000, v27
	v_mov_b32_e32 v87, v26
	s_waitcnt vmcnt(1)
	v_pk_fma_f32 v[26:27], v[42:43], v[28:29], v[108:109] op_sel_hi:[1,0,1]
	v_pk_fma_f32 v[28:29], v[42:43], v[28:29], v[108:109] op_sel_hi:[1,0,1] neg_lo:[0,0,1] neg_hi:[0,0,1]
	v_pk_fma_f32 v[86:87], v[86:87], v[32:33], v[46:47] op_sel_hi:[1,0,1] neg_lo:[0,1,0] neg_hi:[0,1,0]
	v_pk_mul_f32 v[42:43], v[28:29], v[122:123] op_sel_hi:[1,0] neg_lo:[0,1] neg_hi:[0,1]
	v_xor_b32_e32 v46, 0x80000000, v29
	v_mov_b32_e32 v47, v28
	v_pk_fma_f32 v[28:29], v[40:41], v[24:25], v[110:111] op_sel_hi:[1,0,1]
	v_pk_fma_f32 v[24:25], v[40:41], v[24:25], v[110:111] op_sel_hi:[1,0,1] neg_lo:[0,0,1] neg_hi:[0,0,1]
	v_pk_fma_f32 v[42:43], v[46:47], v[120:121], v[42:43] op_sel_hi:[1,0,1] neg_lo:[0,1,0] neg_hi:[0,1,0]
	v_xor_b32_e32 v40, 0x80000000, v25
	v_mov_b32_e32 v41, v24
	v_pk_mul_f32 v[40:41], v[40:41], v[10:11] op_sel_hi:[1,0] neg_lo:[0,1] neg_hi:[0,1]
	s_nop 0
	v_pk_fma_f32 v[88:89], v[24:25], v[10:11], v[40:41] op_sel_hi:[1,0,1] neg_lo:[0,1,0] neg_hi:[0,1,0]
	v_pk_fma_f32 v[24:25], v[34:35], v[22:23], v[112:113] op_sel_hi:[1,0,1]
	v_pk_fma_f32 v[22:23], v[34:35], v[22:23], v[112:113] op_sel_hi:[1,0,1] neg_lo:[0,0,1] neg_hi:[0,0,1]
	v_pk_add_f32 v[40:41], v[84:85], v[38:39]
	v_xor_b32_e32 v34, 0x80000000, v23
	v_mov_b32_e32 v35, v22
	v_pk_mul_f32 v[34:35], v[34:35], v[122:123] op_sel_hi:[1,0] neg_lo:[0,1] neg_hi:[0,1]
	v_pk_add_f32 v[38:39], v[84:85], v[38:39] neg_lo:[0,1] neg_hi:[0,1]
	v_pk_fma_f32 v[90:91], v[22:23], v[120:121], v[34:35] op_sel_hi:[1,0,1] neg_lo:[0,1,0] neg_hi:[0,1,0]
	v_pk_fma_f32 v[22:23], v[66:67], v[20:21], v[114:115] op_sel_hi:[1,0,1]
	v_pk_fma_f32 v[20:21], v[66:67], v[20:21], v[114:115] op_sel_hi:[1,0,1] neg_lo:[0,0,1] neg_hi:[0,0,1]
	v_xor_b32_e32 v46, 0x80000000, v39
	v_xor_b32_e32 v34, 0x80000000, v21
	v_mov_b32_e32 v35, v20
	v_pk_mul_f32 v[34:35], v[34:35], v[36:37] op_sel_hi:[1,0] neg_lo:[0,1] neg_hi:[0,1]
	v_mov_b32_e32 v47, v38
	v_pk_fma_f32 v[66:67], v[20:21], v[32:33], v[34:35] op_sel_hi:[1,0,1] neg_lo:[0,1,0] neg_hi:[0,1,0]
	s_waitcnt vmcnt(0)
	v_pk_fma_f32 v[20:21], v[62:63], v[18:19], v[116:117] op_sel_hi:[1,0,1]
	v_pk_fma_f32 v[18:19], v[62:63], v[18:19], v[116:117] op_sel_hi:[1,0,1] neg_lo:[0,0,1] neg_hi:[0,0,1]
	v_pk_mul_f32 v[46:47], v[46:47], v[36:37] op_sel_hi:[1,0] neg_lo:[0,1] neg_hi:[0,1]
	v_xor_b32_e32 v34, 0x80000000, v19
	v_mov_b32_e32 v35, v18
	v_pk_mul_f32 v[34:35], v[34:35], v[124:125] op_sel_hi:[1,0] neg_lo:[0,1] neg_hi:[0,1]
	v_pk_fma_f32 v[38:39], v[38:39], v[32:33], v[46:47] op_sel_hi:[1,0,1]
	v_pk_add_f32 v[46:47], v[82:83], v[30:31]
	v_pk_add_f32 v[30:31], v[82:83], v[30:31] neg_lo:[0,1] neg_hi:[0,1]
	v_pk_fma_f32 v[62:63], v[18:19], v[118:119], v[34:35] op_sel_hi:[1,0,1] neg_lo:[0,1,0] neg_hi:[0,1,0]
	v_pk_add_f32 v[18:19], v[126:127], v[58:59]
	v_pk_add_f32 v[34:35], v[126:127], v[58:59] neg_lo:[0,1] neg_hi:[0,1]
	v_xor_b32_e32 v58, 0x80000000, v31
	v_mov_b32_e32 v59, v30
	v_pk_mul_f32 v[58:59], v[58:59], v[10:11] op_sel_hi:[1,0] neg_lo:[0,1] neg_hi:[0,1]
	s_nop 0
	v_pk_fma_f32 v[58:59], v[30:31], v[10:11], v[58:59] op_sel_hi:[1,0,1]
	v_pk_add_f32 v[30:31], v[80:81], v[26:27]
	v_pk_add_f32 v[26:27], v[80:81], v[26:27] neg_lo:[0,1] neg_hi:[0,1]
	s_nop 0
	v_pk_mul_f32 v[80:81], v[26:27], v[36:37] op_sel_hi:[1,0]
	v_xor_b32_e32 v82, 0x80000000, v27
	v_mov_b32_e32 v83, v26
	v_pk_add_f32 v[26:27], v[76:77], v[28:29]
	v_pk_add_f32 v[28:29], v[76:77], v[28:29] neg_lo:[0,1] neg_hi:[0,1]
	v_pk_fma_f32 v[80:81], v[82:83], v[32:33], v[80:81] op_sel_hi:[1,0,1] neg_lo:[0,1,0] neg_hi:[0,1,0]
	v_xor_b32_e32 v77, 0x80000000, v28
	v_mov_b32_e32 v76, v29
	v_pk_add_f32 v[28:29], v[70:71], v[24:25]
	v_pk_add_f32 v[24:25], v[70:71], v[24:25] neg_lo:[0,1] neg_hi:[0,1]
	s_nop 0
	v_pk_mul_f32 v[70:71], v[24:25], v[36:37] op_sel_hi:[1,0] neg_lo:[0,1] neg_hi:[0,1]
	v_xor_b32_e32 v82, 0x80000000, v25
	v_mov_b32_e32 v83, v24
	v_pk_fma_f32 v[24:25], v[82:83], v[32:33], v[70:71] op_sel_hi:[1,0,1] neg_lo:[0,1,0] neg_hi:[0,1,0]
	v_pk_add_f32 v[70:71], v[50:51], v[22:23]
	v_pk_add_f32 v[22:23], v[50:51], v[22:23] neg_lo:[0,1] neg_hi:[0,1]
	s_nop 0
	v_xor_b32_e32 v50, 0x80000000, v23
	v_mov_b32_e32 v51, v22
	v_pk_mul_f32 v[50:51], v[50:51], v[10:11] op_sel_hi:[1,0] neg_lo:[0,1] neg_hi:[0,1]
	s_nop 0
	v_pk_fma_f32 v[50:51], v[22:23], v[10:11], v[50:51] op_sel_hi:[1,0,1] neg_lo:[0,1,0] neg_hi:[0,1,0]
	v_pk_add_f32 v[22:23], v[44:45], v[20:21]
	v_pk_add_f32 v[20:21], v[44:45], v[20:21] neg_lo:[0,1] neg_hi:[0,1]
	s_nop 0
	v_xor_b32_e32 v44, 0x80000000, v21
	v_mov_b32_e32 v45, v20
	v_pk_mul_f32 v[44:45], v[44:45], v[36:37] op_sel_hi:[1,0] neg_lo:[0,1] neg_hi:[0,1]
	s_nop 0
	v_pk_fma_f32 v[20:21], v[20:21], v[32:33], v[44:45] op_sel_hi:[1,0,1] neg_lo:[0,1,0] neg_hi:[0,1,0]
	v_pk_add_f32 v[44:45], v[18:19], v[26:27]
	v_pk_add_f32 v[18:19], v[18:19], v[26:27] neg_lo:[0,1] neg_hi:[0,1]
	v_pk_add_f32 v[26:27], v[40:41], v[28:29]
	v_pk_add_f32 v[28:29], v[40:41], v[28:29] neg_lo:[0,1] neg_hi:[0,1]
	s_nop 0
	v_xor_b32_e32 v40, 0x80000000, v29
	v_mov_b32_e32 v41, v28
	v_pk_mul_f32 v[40:41], v[40:41], v[10:11] op_sel_hi:[1,0] neg_lo:[0,1] neg_hi:[0,1]
	s_nop 0
	v_pk_fma_f32 v[28:29], v[28:29], v[10:11], v[40:41] op_sel_hi:[1,0,1]
	v_pk_add_f32 v[40:41], v[46:47], v[70:71]
	v_pk_add_f32 v[46:47], v[46:47], v[70:71] neg_lo:[0,1] neg_hi:[0,1]
	s_nop 0
	v_xor_b32_e32 v71, 0x80000000, v46
	v_mov_b32_e32 v70, v47
	v_pk_add_f32 v[46:47], v[30:31], v[22:23]
	v_pk_add_f32 v[22:23], v[30:31], v[22:23] neg_lo:[0,1] neg_hi:[0,1]
	s_nop 0
	v_xor_b32_e32 v30, 0x80000000, v23
	v_mov_b32_e32 v31, v22
	v_pk_mul_f32 v[30:31], v[30:31], v[10:11] op_sel_hi:[1,0] neg_lo:[0,1] neg_hi:[0,1]
	s_nop 0
	v_pk_fma_f32 v[82:83], v[22:23], v[10:11], v[30:31] op_sel_hi:[1,0,1] neg_lo:[0,1,0] neg_hi:[0,1,0]
	v_pk_add_f32 v[30:31], v[26:27], v[46:47]
	v_pk_add_f32 v[26:27], v[26:27], v[46:47] neg_lo:[0,1] neg_hi:[0,1]
	v_pk_add_f32 v[22:23], v[44:45], v[40:41]
	v_pk_add_f32 v[40:41], v[44:45], v[40:41] neg_lo:[0,1] neg_hi:[0,1]
	v_xor_b32_e32 v45, 0x80000000, v26
	v_mov_b32_e32 v44, v27
	v_pk_add_f32 v[84:85], v[22:23], v[30:31]
	v_pk_add_f32 v[30:31], v[22:23], v[30:31] neg_lo:[0,1] neg_hi:[0,1]
	v_pk_add_f32 v[46:47], v[40:41], v[44:45]
	v_pk_add_f32 v[22:23], v[40:41], v[44:45] neg_lo:[0,1] neg_hi:[0,1]
	v_pk_add_f32 v[40:41], v[28:29], v[82:83]
	v_pk_add_f32 v[28:29], v[28:29], v[82:83] neg_lo:[0,1] neg_hi:[0,1]
	v_pk_add_f32 v[26:27], v[18:19], v[70:71]
	v_pk_add_f32 v[18:19], v[18:19], v[70:71] neg_lo:[0,1] neg_hi:[0,1]
	v_xor_b32_e32 v45, 0x80000000, v28
	v_mov_b32_e32 v44, v29
	v_pk_add_f32 v[70:71], v[26:27], v[40:41]
	v_pk_add_f32 v[26:27], v[26:27], v[40:41] neg_lo:[0,1] neg_hi:[0,1]
	v_pk_add_f32 v[40:41], v[18:19], v[44:45]
	v_pk_add_f32 v[18:19], v[18:19], v[44:45] neg_lo:[0,1] neg_hi:[0,1]
	v_pk_add_f32 v[28:29], v[34:35], v[76:77]
	v_pk_add_f32 v[44:45], v[34:35], v[76:77] neg_lo:[0,1] neg_hi:[0,1]
	v_pk_add_f32 v[34:35], v[38:39], v[24:25]
	v_pk_add_f32 v[24:25], v[38:39], v[24:25] neg_lo:[0,1] neg_hi:[0,1]
	s_nop 0
	v_xor_b32_e32 v38, 0x80000000, v25
	v_mov_b32_e32 v39, v24
	v_pk_mul_f32 v[38:39], v[10:11], v[38:39] op_sel_hi:[0,1] neg_lo:[1,0] neg_hi:[1,0]
	v_pk_fma_f32 v[38:39], v[10:11], v[24:25], v[38:39] op_sel_hi:[0,1,1]
	v_pk_add_f32 v[24:25], v[58:59], v[50:51]
	v_pk_add_f32 v[50:51], v[58:59], v[50:51] neg_lo:[0,1] neg_hi:[0,1]
	s_nop 0
	v_xor_b32_e32 v59, 0x80000000, v50
	v_mov_b32_e32 v58, v51
	v_pk_add_f32 v[50:51], v[80:81], v[20:21]
	v_pk_add_f32 v[20:21], v[80:81], v[20:21] neg_lo:[0,1] neg_hi:[0,1]
	s_nop 0
	v_xor_b32_e32 v76, 0x80000000, v21
	v_mov_b32_e32 v77, v20
	v_pk_mul_f32 v[76:77], v[10:11], v[76:77] op_sel_hi:[0,1] neg_lo:[1,0] neg_hi:[1,0]
	v_pk_fma_f32 v[20:21], v[10:11], v[20:21], v[76:77] op_sel_hi:[0,1,1] neg_lo:[1,0,0] neg_hi:[1,0,0]
	v_pk_add_f32 v[76:77], v[28:29], v[24:25]
	v_pk_add_f32 v[24:25], v[28:29], v[24:25] neg_lo:[0,1] neg_hi:[0,1]
	v_pk_add_f32 v[28:29], v[34:35], v[50:51]
	v_pk_add_f32 v[34:35], v[34:35], v[50:51] neg_lo:[0,1] neg_hi:[0,1]
	v_pk_add_f32 v[82:83], v[76:77], v[28:29]
	v_xor_b32_e32 v81, 0x80000000, v34
	v_mov_b32_e32 v80, v35
	v_pk_add_f32 v[34:35], v[76:77], v[28:29] neg_lo:[0,1] neg_hi:[0,1]
	v_pk_add_f32 v[28:29], v[44:45], v[58:59]
	v_pk_add_f32 v[58:59], v[44:45], v[58:59] neg_lo:[0,1] neg_hi:[0,1]
	v_pk_add_f32 v[44:45], v[38:39], v[20:21]
	v_pk_add_f32 v[20:21], v[38:39], v[20:21] neg_lo:[0,1] neg_hi:[0,1]
	v_pk_add_f32 v[76:77], v[28:29], v[44:45]
	v_xor_b32_e32 v39, 0x80000000, v20
	v_mov_b32_e32 v38, v21
	v_pk_add_f32 v[28:29], v[28:29], v[44:45] neg_lo:[0,1] neg_hi:[0,1]
	v_pk_add_f32 v[44:45], v[58:59], v[38:39]
	v_pk_add_f32 v[20:21], v[58:59], v[38:39] neg_lo:[0,1] neg_hi:[0,1]
	v_pk_add_f32 v[38:39], v[74:75], v[54:55]
	v_pk_add_f32 v[58:59], v[74:75], v[54:55] neg_lo:[0,1] neg_hi:[0,1]
	v_pk_add_f32 v[54:55], v[78:79], v[52:53]
	v_pk_add_f32 v[52:53], v[78:79], v[52:53] neg_lo:[0,1] neg_hi:[0,1]
	v_pk_add_f32 v[50:51], v[24:25], v[80:81]
	v_xor_b32_e32 v74, 0x80000000, v53
	v_mov_b32_e32 v75, v52
	v_pk_mul_f32 v[74:75], v[36:37], v[74:75] op_sel_hi:[0,1] neg_lo:[1,0] neg_hi:[1,0]
	v_pk_fma_f32 v[52:53], v[32:33], v[52:53], v[74:75] op_sel_hi:[0,1,1]
	v_pk_add_f32 v[74:75], v[72:73], v[86:87]
	v_pk_add_f32 v[72:73], v[72:73], v[86:87] neg_lo:[0,1] neg_hi:[0,1]
	v_pk_add_f32 v[24:25], v[24:25], v[80:81] neg_lo:[0,1] neg_hi:[0,1]
	v_xor_b32_e32 v78, 0x80000000, v73
	v_mov_b32_e32 v79, v72
	v_pk_mul_f32 v[78:79], v[10:11], v[78:79] op_sel_hi:[0,1] neg_lo:[1,0] neg_hi:[1,0]
	v_pk_fma_f32 v[72:73], v[10:11], v[72:73], v[78:79] op_sel_hi:[0,1,1]
	v_pk_add_f32 v[78:79], v[68:69], v[42:43]
	v_pk_add_f32 v[42:43], v[68:69], v[42:43] neg_lo:[0,1] neg_hi:[0,1]
	s_nop 0
	v_xor_b32_e32 v68, 0x80000000, v43
	v_mov_b32_e32 v69, v42
	v_pk_mul_f32 v[68:69], v[32:33], v[68:69] op_sel_hi:[0,1] neg_lo:[1,0] neg_hi:[1,0]
	v_pk_fma_f32 v[42:43], v[36:37], v[42:43], v[68:69] op_sel_hi:[0,1,1]
	v_pk_add_f32 v[68:69], v[56:57], v[88:89]
	v_pk_add_f32 v[56:57], v[56:57], v[88:89] neg_lo:[0,1] neg_hi:[0,1]
	s_nop 0
	v_xor_b32_e32 v81, 0x80000000, v56
	v_mov_b32_e32 v80, v57
	v_pk_add_f32 v[56:57], v[64:65], v[90:91]
	v_pk_add_f32 v[64:65], v[64:65], v[90:91] neg_lo:[0,1] neg_hi:[0,1]
	s_nop 0
	v_xor_b32_e32 v86, 0x80000000, v65
	v_mov_b32_e32 v87, v64
	v_pk_mul_f32 v[86:87], v[32:33], v[86:87] op_sel_hi:[0,1] neg_lo:[1,0] neg_hi:[1,0]
	v_pk_fma_f32 v[64:65], v[36:37], v[64:65], v[86:87] op_sel_hi:[0,1,1] neg_lo:[1,0,0] neg_hi:[1,0,0]
	v_pk_add_f32 v[86:87], v[60:61], v[66:67]
	v_pk_add_f32 v[60:61], v[60:61], v[66:67] neg_lo:[0,1] neg_hi:[0,1]
	s_nop 0
	v_xor_b32_e32 v66, 0x80000000, v61
	v_mov_b32_e32 v67, v60
	v_pk_mul_f32 v[66:67], v[10:11], v[66:67] op_sel_hi:[0,1] neg_lo:[1,0] neg_hi:[1,0]
	v_pk_fma_f32 v[60:61], v[10:11], v[60:61], v[66:67] op_sel_hi:[0,1,1] neg_lo:[1,0,0] neg_hi:[1,0,0]
	v_pk_add_f32 v[66:67], v[48:49], v[62:63]
	v_pk_add_f32 v[48:49], v[48:49], v[62:63] neg_lo:[0,1] neg_hi:[0,1]
	s_nop 0
	v_xor_b32_e32 v62, 0x80000000, v49
	v_mov_b32_e32 v63, v48
	v_pk_mul_f32 v[36:37], v[36:37], v[62:63] op_sel_hi:[0,1] neg_lo:[1,0] neg_hi:[1,0]
	v_pk_fma_f32 v[36:37], v[32:33], v[48:49], v[36:37] op_sel_hi:[0,1,1] neg_lo:[1,0,0] neg_hi:[1,0,0]
	v_pk_add_f32 v[32:33], v[38:39], v[68:69]
	v_pk_add_f32 v[48:49], v[38:39], v[68:69] neg_lo:[0,1] neg_hi:[0,1]
	v_pk_add_f32 v[38:39], v[56:57], v[54:55]
	v_pk_add_f32 v[54:55], v[54:55], v[56:57] neg_lo:[0,1] neg_hi:[0,1]
	v_pk_add_f32 v[62:63], v[74:75], v[86:87] neg_lo:[0,1] neg_hi:[0,1]
	v_xor_b32_e32 v56, 0x80000000, v55
	v_mov_b32_e32 v57, v54
	v_pk_mul_f32 v[56:57], v[10:11], v[56:57] op_sel_hi:[0,1] neg_lo:[1,0] neg_hi:[1,0]
	v_xor_b32_e32 v69, 0x80000000, v62
	v_mov_b32_e32 v68, v63
	v_pk_add_f32 v[62:63], v[78:79], v[66:67]
	v_pk_add_f32 v[66:67], v[78:79], v[66:67] neg_lo:[0,1] neg_hi:[0,1]
	v_pk_fma_f32 v[56:57], v[10:11], v[54:55], v[56:57] op_sel_hi:[0,1,1]
	v_pk_add_f32 v[54:55], v[74:75], v[86:87]
	v_xor_b32_e32 v74, 0x80000000, v67
	v_mov_b32_e32 v75, v66
	v_pk_mul_f32 v[74:75], v[10:11], v[74:75] op_sel_hi:[0,1] neg_lo:[1,0] neg_hi:[1,0]
	v_pk_fma_f32 v[66:67], v[10:11], v[66:67], v[74:75] op_sel_hi:[0,1,1] neg_lo:[1,0,0] neg_hi:[1,0,0]
	v_pk_add_f32 v[74:75], v[32:33], v[54:55]
	v_pk_add_f32 v[32:33], v[32:33], v[54:55] neg_lo:[0,1] neg_hi:[0,1]
	v_pk_add_f32 v[54:55], v[38:39], v[62:63]
	v_pk_add_f32 v[38:39], v[38:39], v[62:63] neg_lo:[0,1] neg_hi:[0,1]
	v_pk_add_f32 v[78:79], v[74:75], v[54:55]
	v_xor_b32_e32 v63, 0x80000000, v38
	v_mov_b32_e32 v62, v39
	v_pk_add_f32 v[54:55], v[74:75], v[54:55] neg_lo:[0,1] neg_hi:[0,1]
	v_pk_add_f32 v[74:75], v[32:33], v[62:63]
	v_pk_add_f32 v[38:39], v[32:33], v[62:63] neg_lo:[0,1] neg_hi:[0,1]
	v_pk_add_f32 v[32:33], v[48:49], v[68:69]
	v_pk_add_f32 v[62:63], v[48:49], v[68:69] neg_lo:[0,1] neg_hi:[0,1]
	v_pk_add_f32 v[48:49], v[56:57], v[66:67]
	v_pk_add_f32 v[56:57], v[56:57], v[66:67] neg_lo:[0,1] neg_hi:[0,1]
	s_nop 0
	v_xor_b32_e32 v67, 0x80000000, v56
	v_mov_b32_e32 v66, v57
	v_pk_add_f32 v[56:57], v[32:33], v[48:49]
	v_pk_add_f32 v[48:49], v[32:33], v[48:49] neg_lo:[0,1] neg_hi:[0,1]
	v_pk_add_f32 v[68:69], v[62:63], v[66:67]
	v_pk_add_f32 v[32:33], v[62:63], v[66:67] neg_lo:[0,1] neg_hi:[0,1]
	v_pk_add_f32 v[66:67], v[64:65], v[52:53]
	v_pk_add_f32 v[52:53], v[52:53], v[64:65] neg_lo:[0,1] neg_hi:[0,1]
	v_pk_add_f32 v[62:63], v[58:59], v[80:81]
	v_xor_b32_e32 v64, 0x80000000, v53
	v_mov_b32_e32 v65, v52
	v_pk_mul_f32 v[64:65], v[10:11], v[64:65] op_sel_hi:[0,1] neg_lo:[1,0] neg_hi:[1,0]
	v_pk_fma_f32 v[52:53], v[10:11], v[52:53], v[64:65] op_sel_hi:[0,1,1]
	v_pk_add_f32 v[64:65], v[72:73], v[60:61]
	v_pk_add_f32 v[60:61], v[72:73], v[60:61] neg_lo:[0,1] neg_hi:[0,1]
	v_pk_add_f32 v[58:59], v[58:59], v[80:81] neg_lo:[0,1] neg_hi:[0,1]
	v_xor_b32_e32 v73, 0x80000000, v60
	v_mov_b32_e32 v72, v61
	v_pk_add_f32 v[60:61], v[42:43], v[36:37]
	v_pk_add_f32 v[36:37], v[42:43], v[36:37] neg_lo:[0,1] neg_hi:[0,1]
	s_nop 0
	v_xor_b32_e32 v42, 0x80000000, v37
	v_mov_b32_e32 v43, v36
	v_pk_mul_f32 v[42:43], v[10:11], v[42:43] op_sel_hi:[0,1] neg_lo:[1,0] neg_hi:[1,0]
	v_pk_fma_f32 v[36:37], v[10:11], v[36:37], v[42:43] op_sel_hi:[0,1,1] neg_lo:[1,0,0] neg_hi:[1,0,0]
	v_pk_add_f32 v[42:43], v[62:63], v[64:65]
	v_pk_add_f32 v[62:63], v[62:63], v[64:65] neg_lo:[0,1] neg_hi:[0,1]
	v_pk_add_f32 v[64:65], v[66:67], v[60:61]
	v_pk_add_f32 v[60:61], v[66:67], v[60:61] neg_lo:[0,1] neg_hi:[0,1]
	v_lshl_add_u32 v10, v13, 3, 0
	v_xor_b32_e32 v67, 0x80000000, v60
	v_mov_b32_e32 v66, v61
	v_pk_add_f32 v[60:61], v[42:43], v[64:65]
	v_pk_add_f32 v[64:65], v[42:43], v[64:65] neg_lo:[0,1] neg_hi:[0,1]
	v_pk_add_f32 v[80:81], v[62:63], v[66:67]
	v_pk_add_f32 v[42:43], v[62:63], v[66:67] neg_lo:[0,1] neg_hi:[0,1]
	v_pk_add_f32 v[66:67], v[52:53], v[36:37]
	v_pk_add_f32 v[36:37], v[52:53], v[36:37] neg_lo:[0,1] neg_hi:[0,1]
	v_pk_add_f32 v[62:63], v[58:59], v[72:73]
	v_pk_add_f32 v[58:59], v[58:59], v[72:73] neg_lo:[0,1] neg_hi:[0,1]
	v_xor_b32_e32 v73, 0x80000000, v36
	v_mov_b32_e32 v72, v37
	v_pk_add_f32 v[86:87], v[62:63], v[66:67]
	v_pk_add_f32 v[52:53], v[62:63], v[66:67] neg_lo:[0,1] neg_hi:[0,1]
	v_pk_add_f32 v[62:63], v[58:59], v[72:73]
	v_pk_add_f32 v[36:37], v[58:59], v[72:73] neg_lo:[0,1] neg_hi:[0,1]
	v_xor_b32_e32 v58, 0x80000000, v85
	v_mov_b32_e32 v59, v85
	v_pk_mul_f32 v[58:59], v[58:59], s[14:15]
	v_xor_b32_e32 v66, 0x80000000, v79
	v_pk_fma_f32 v[58:59], v[84:85], s[94:95], v[58:59] op_sel_hi:[0,1,1]
	ds_write_b64 v10, v[58:59]
	v_pk_fma_f32 v[58:59], v[16:17], s[90:91], v[16:17] op_sel:[1,0,0] op_sel_hi:[0,1,1]
	v_mov_b32_e32 v67, v79
	v_pk_mul_f32 v[66:67], v[58:59], v[66:67] op_sel:[1,0] op_sel_hi:[0,1]
	v_pk_fma_f32 v[66:67], v[58:59], v[78:79], v[66:67] op_sel_hi:[1,0,1]
	ds_write_b64 v10, v[66:67] offset:4224
	v_xor_b32_e32 v66, 0x80000000, v59
	v_mov_b32_e32 v67, v59
	v_pk_mul_f32 v[66:67], v[16:17], v[66:67] op_sel:[1,0] op_sel_hi:[0,1]
	v_pk_fma_f32 v[58:59], v[16:17], v[58:59], v[66:67] op_sel_hi:[1,0,1]
	v_xor_b32_e32 v66, 0x80000000, v83
	v_mov_b32_e32 v67, v83
	v_pk_mul_f32 v[66:67], v[58:59], v[66:67] op_sel:[1,0] op_sel_hi:[0,1]
	v_pk_fma_f32 v[66:67], v[58:59], v[82:83], v[66:67] op_sel_hi:[1,0,1]
	ds_write_b64 v10, v[66:67] offset:8448
	v_xor_b32_e32 v66, 0x80000000, v59
	v_mov_b32_e32 v67, v59
	v_pk_mul_f32 v[66:67], v[16:17], v[66:67] op_sel:[1,0] op_sel_hi:[0,1]
	v_pk_fma_f32 v[58:59], v[16:17], v[58:59], v[66:67] op_sel_hi:[1,0,1]
	v_xor_b32_e32 v66, 0x80000000, v61
	v_mov_b32_e32 v67, v61
	v_pk_mul_f32 v[66:67], v[58:59], v[66:67] op_sel:[1,0] op_sel_hi:[0,1]
	v_pk_fma_f32 v[60:61], v[58:59], v[60:61], v[66:67] op_sel_hi:[1,0,1]
	ds_write_b64 v10, v[60:61] offset:12672
	v_xor_b32_e32 v60, 0x80000000, v59
	v_mov_b32_e32 v61, v59
	v_pk_mul_f32 v[60:61], v[16:17], v[60:61] op_sel:[1,0] op_sel_hi:[0,1]
	v_pk_fma_f32 v[58:59], v[16:17], v[58:59], v[60:61] op_sel_hi:[1,0,1]
	v_xor_b32_e32 v60, 0x80000000, v71
	v_mov_b32_e32 v61, v71
	v_pk_mul_f32 v[60:61], v[60:61], v[58:59] op_sel:[0,1] op_sel_hi:[1,0]
	s_nop 0
	v_pk_fma_f32 v[60:61], v[70:71], v[58:59], v[60:61] op_sel_hi:[0,1,1]
	ds_write_b64 v10, v[60:61] offset:16896
	v_xor_b32_e32 v60, 0x80000000, v59
	v_mov_b32_e32 v61, v59
	v_pk_mul_f32 v[60:61], v[16:17], v[60:61] op_sel:[1,0] op_sel_hi:[0,1]
	v_pk_fma_f32 v[58:59], v[16:17], v[58:59], v[60:61] op_sel_hi:[1,0,1]
	v_xor_b32_e32 v60, 0x80000000, v57
	v_mov_b32_e32 v61, v57
	v_pk_mul_f32 v[60:61], v[58:59], v[60:61] op_sel:[1,0] op_sel_hi:[0,1]
	v_pk_fma_f32 v[56:57], v[58:59], v[56:57], v[60:61] op_sel_hi:[1,0,1]
	ds_write_b64 v10, v[56:57] offset:21120
	v_xor_b32_e32 v56, 0x80000000, v59
	v_mov_b32_e32 v57, v59
	v_pk_mul_f32 v[56:57], v[16:17], v[56:57] op_sel:[1,0] op_sel_hi:[0,1]
	v_pk_fma_f32 v[56:57], v[16:17], v[58:59], v[56:57] op_sel_hi:[1,0,1]
	v_xor_b32_e32 v58, 0x80000000, v77
	v_mov_b32_e32 v59, v77
	v_pk_mul_f32 v[58:59], v[58:59], v[56:57] op_sel:[0,1] op_sel_hi:[1,0]
	s_nop 0
	v_pk_fma_f32 v[58:59], v[76:77], v[56:57], v[58:59] op_sel_hi:[0,1,1]
	ds_write_b64 v10, v[58:59] offset:25344
	v_xor_b32_e32 v58, 0x80000000, v57
	v_mov_b32_e32 v59, v57
	v_pk_mul_f32 v[58:59], v[16:17], v[58:59] op_sel:[1,0] op_sel_hi:[0,1]
	v_pk_fma_f32 v[56:57], v[16:17], v[56:57], v[58:59] op_sel_hi:[1,0,1]
	v_xor_b32_e32 v58, 0x80000000, v87
	v_mov_b32_e32 v59, v87
	v_pk_mul_f32 v[58:59], v[58:59], v[56:57] op_sel:[0,1] op_sel_hi:[1,0]
	s_nop 0
	v_pk_fma_f32 v[58:59], v[86:87], v[56:57], v[58:59] op_sel_hi:[0,1,1]
	ds_write_b64 v10, v[58:59] offset:29568
	v_xor_b32_e32 v58, 0x80000000, v57
	v_mov_b32_e32 v59, v57
	v_pk_mul_f32 v[58:59], v[16:17], v[58:59] op_sel:[1,0] op_sel_hi:[0,1]
	v_pk_fma_f32 v[56:57], v[16:17], v[56:57], v[58:59] op_sel_hi:[1,0,1]
	v_xor_b32_e32 v58, 0x80000000, v47
	v_mov_b32_e32 v59, v47
	v_pk_mul_f32 v[58:59], v[58:59], v[56:57] op_sel:[0,1] op_sel_hi:[1,0]
	s_nop 0
	v_pk_fma_f32 v[46:47], v[46:47], v[56:57], v[58:59] op_sel_hi:[0,1,1]
	ds_write_b64 v10, v[46:47] offset:33792
	v_xor_b32_e32 v46, 0x80000000, v57
	v_mov_b32_e32 v47, v57
	v_pk_mul_f32 v[46:47], v[16:17], v[46:47] op_sel:[1,0] op_sel_hi:[0,1]
	v_pk_fma_f32 v[46:47], v[16:17], v[56:57], v[46:47] op_sel_hi:[1,0,1]
	v_xor_b32_e32 v56, 0x80000000, v75
	v_mov_b32_e32 v57, v75
	v_pk_mul_f32 v[56:57], v[56:57], v[46:47] op_sel:[0,1] op_sel_hi:[1,0]
	s_nop 0
	v_pk_fma_f32 v[56:57], v[74:75], v[46:47], v[56:57] op_sel_hi:[0,1,1]
	ds_write_b64 v10, v[56:57] offset:38016
	v_xor_b32_e32 v56, 0x80000000, v47
	v_mov_b32_e32 v57, v47
	v_pk_mul_f32 v[56:57], v[16:17], v[56:57] op_sel:[1,0] op_sel_hi:[0,1]
	v_pk_fma_f32 v[46:47], v[16:17], v[46:47], v[56:57] op_sel_hi:[1,0,1]
	v_xor_b32_e32 v56, 0x80000000, v51
	v_mov_b32_e32 v57, v51
	v_pk_mul_f32 v[56:57], v[56:57], v[46:47] op_sel:[0,1] op_sel_hi:[1,0]
	s_nop 0
	v_pk_fma_f32 v[50:51], v[50:51], v[46:47], v[56:57] op_sel_hi:[0,1,1]
	ds_write_b64 v10, v[50:51] offset:42240
	v_xor_b32_e32 v50, 0x80000000, v47
	v_mov_b32_e32 v51, v47
	v_pk_mul_f32 v[50:51], v[16:17], v[50:51] op_sel:[1,0] op_sel_hi:[0,1]
	v_pk_fma_f32 v[46:47], v[16:17], v[46:47], v[50:51] op_sel_hi:[1,0,1]
	v_xor_b32_e32 v50, 0x80000000, v81
	v_mov_b32_e32 v51, v81
	v_pk_mul_f32 v[50:51], v[50:51], v[46:47] op_sel:[0,1] op_sel_hi:[1,0]
	s_nop 0
	v_pk_fma_f32 v[50:51], v[80:81], v[46:47], v[50:51] op_sel_hi:[0,1,1]
	ds_write_b64 v10, v[50:51] offset:46464
	v_xor_b32_e32 v50, 0x80000000, v47
	v_mov_b32_e32 v51, v47
	v_pk_mul_f32 v[50:51], v[16:17], v[50:51] op_sel:[1,0] op_sel_hi:[0,1]
	v_pk_fma_f32 v[46:47], v[16:17], v[46:47], v[50:51] op_sel_hi:[1,0,1]
	v_xor_b32_e32 v50, 0x80000000, v41
	v_mov_b32_e32 v51, v41
	v_pk_mul_f32 v[50:51], v[50:51], v[46:47] op_sel:[0,1] op_sel_hi:[1,0]
	s_nop 0
	v_pk_fma_f32 v[40:41], v[40:41], v[46:47], v[50:51] op_sel_hi:[0,1,1]
	ds_write_b64 v10, v[40:41] offset:50688
	v_xor_b32_e32 v40, 0x80000000, v47
	v_mov_b32_e32 v41, v47
	v_pk_mul_f32 v[40:41], v[16:17], v[40:41] op_sel:[1,0] op_sel_hi:[0,1]
	v_pk_fma_f32 v[40:41], v[16:17], v[46:47], v[40:41] op_sel_hi:[1,0,1]
	v_xor_b32_e32 v46, 0x80000000, v69
	v_mov_b32_e32 v47, v69
	v_pk_mul_f32 v[46:47], v[46:47], v[40:41] op_sel:[0,1] op_sel_hi:[1,0]
	s_nop 0
	v_pk_fma_f32 v[46:47], v[68:69], v[40:41], v[46:47] op_sel_hi:[0,1,1]
	ds_write_b64 v10, v[46:47] offset:54912
	v_xor_b32_e32 v46, 0x80000000, v41
	v_mov_b32_e32 v47, v41
	v_pk_mul_f32 v[46:47], v[16:17], v[46:47] op_sel:[1,0] op_sel_hi:[0,1]
	v_pk_fma_f32 v[40:41], v[16:17], v[40:41], v[46:47] op_sel_hi:[1,0,1]
	v_xor_b32_e32 v46, 0x80000000, v45
	v_mov_b32_e32 v47, v45
	v_pk_mul_f32 v[46:47], v[46:47], v[40:41] op_sel:[0,1] op_sel_hi:[1,0]
	s_nop 0
	v_pk_fma_f32 v[44:45], v[44:45], v[40:41], v[46:47] op_sel_hi:[0,1,1]
	ds_write_b64 v10, v[44:45] offset:59136
	v_xor_b32_e32 v44, 0x80000000, v41
	v_mov_b32_e32 v45, v41
	v_pk_mul_f32 v[44:45], v[16:17], v[44:45] op_sel:[1,0] op_sel_hi:[0,1]
	v_pk_fma_f32 v[40:41], v[16:17], v[40:41], v[44:45] op_sel_hi:[1,0,1]
	v_xor_b32_e32 v44, 0x80000000, v63
	v_mov_b32_e32 v45, v63
	v_pk_mul_f32 v[44:45], v[44:45], v[40:41] op_sel:[0,1] op_sel_hi:[1,0]
	s_nop 0
	v_pk_fma_f32 v[44:45], v[62:63], v[40:41], v[44:45] op_sel_hi:[0,1,1]
	ds_write_b64 v10, v[44:45] offset:63360
	v_xor_b32_e32 v44, 0x80000000, v41
	v_mov_b32_e32 v45, v41
	v_pk_mul_f32 v[44:45], v[16:17], v[44:45] op_sel:[1,0] op_sel_hi:[0,1]
	v_pk_fma_f32 v[40:41], v[16:17], v[40:41], v[44:45] op_sel_hi:[1,0,1]
	v_xor_b32_e32 v44, 0x80000000, v31
	v_mov_b32_e32 v45, v31
	v_pk_mul_f32 v[44:45], v[44:45], v[40:41] op_sel:[0,1] op_sel_hi:[1,0]
	v_add_u32_e32 v13, 0x10800, v10
	v_pk_fma_f32 v[30:31], v[30:31], v[40:41], v[44:45] op_sel_hi:[0,1,1]
	ds_write_b64 v13, v[30:31]
	v_xor_b32_e32 v30, 0x80000000, v41
	v_mov_b32_e32 v31, v41
	v_pk_mul_f32 v[30:31], v[16:17], v[30:31] op_sel:[1,0] op_sel_hi:[0,1]
	v_pk_fma_f32 v[30:31], v[16:17], v[40:41], v[30:31] op_sel_hi:[1,0,1]
	v_xor_b32_e32 v40, 0x80000000, v55
	v_mov_b32_e32 v41, v55
	v_pk_mul_f32 v[40:41], v[40:41], v[30:31] op_sel:[0,1] op_sel_hi:[1,0]
	v_add_u32_e32 v13, 0x11880, v10
	v_pk_fma_f32 v[40:41], v[54:55], v[30:31], v[40:41] op_sel_hi:[0,1,1]
	ds_write_b64 v13, v[40:41]
	v_xor_b32_e32 v40, 0x80000000, v31
	v_mov_b32_e32 v41, v31
	v_pk_mul_f32 v[40:41], v[16:17], v[40:41] op_sel:[1,0] op_sel_hi:[0,1]
	v_pk_fma_f32 v[30:31], v[16:17], v[30:31], v[40:41] op_sel_hi:[1,0,1]
	v_xor_b32_e32 v40, 0x80000000, v35
	v_mov_b32_e32 v41, v35
	v_pk_mul_f32 v[40:41], v[40:41], v[30:31] op_sel:[0,1] op_sel_hi:[1,0]
	v_add_u32_e32 v13, 0x12900, v10
	v_pk_fma_f32 v[34:35], v[34:35], v[30:31], v[40:41] op_sel_hi:[0,1,1]
	ds_write_b64 v13, v[34:35]
	v_xor_b32_e32 v34, 0x80000000, v31
	v_mov_b32_e32 v35, v31
	v_pk_mul_f32 v[34:35], v[16:17], v[34:35] op_sel:[1,0] op_sel_hi:[0,1]
	v_pk_fma_f32 v[30:31], v[16:17], v[30:31], v[34:35] op_sel_hi:[1,0,1]
	v_xor_b32_e32 v34, 0x80000000, v65
	v_mov_b32_e32 v35, v65
	v_pk_mul_f32 v[34:35], v[34:35], v[30:31] op_sel:[0,1] op_sel_hi:[1,0]
	v_add_u32_e32 v13, 0x13980, v10
	v_pk_fma_f32 v[34:35], v[64:65], v[30:31], v[34:35] op_sel_hi:[0,1,1]
	ds_write_b64 v13, v[34:35]
	v_xor_b32_e32 v34, 0x80000000, v31
	v_mov_b32_e32 v35, v31
	v_pk_mul_f32 v[34:35], v[16:17], v[34:35] op_sel:[1,0] op_sel_hi:[0,1]
	v_pk_fma_f32 v[30:31], v[16:17], v[30:31], v[34:35] op_sel_hi:[1,0,1]
	v_xor_b32_e32 v34, 0x80000000, v27
	v_mov_b32_e32 v35, v27
	v_pk_mul_f32 v[34:35], v[34:35], v[30:31] op_sel:[0,1] op_sel_hi:[1,0]
	v_add_u32_e32 v13, 0x14a00, v10
	v_pk_fma_f32 v[26:27], v[26:27], v[30:31], v[34:35] op_sel_hi:[0,1,1]
	ds_write_b64 v13, v[26:27]
	v_xor_b32_e32 v26, 0x80000000, v31
	v_mov_b32_e32 v27, v31
	v_pk_mul_f32 v[26:27], v[16:17], v[26:27] op_sel:[1,0] op_sel_hi:[0,1]
	v_pk_fma_f32 v[26:27], v[16:17], v[30:31], v[26:27] op_sel_hi:[1,0,1]
	v_xor_b32_e32 v30, 0x80000000, v49
	v_mov_b32_e32 v31, v49
	v_pk_mul_f32 v[30:31], v[30:31], v[26:27] op_sel:[0,1] op_sel_hi:[1,0]
	v_add_u32_e32 v13, 0x15a80, v10
	v_pk_fma_f32 v[30:31], v[48:49], v[26:27], v[30:31] op_sel_hi:[0,1,1]
	ds_write_b64 v13, v[30:31]
	v_xor_b32_e32 v30, 0x80000000, v27
	v_mov_b32_e32 v31, v27
	v_pk_mul_f32 v[30:31], v[16:17], v[30:31] op_sel:[1,0] op_sel_hi:[0,1]
	v_pk_fma_f32 v[26:27], v[16:17], v[26:27], v[30:31] op_sel_hi:[1,0,1]
	v_xor_b32_e32 v30, 0x80000000, v29
	v_mov_b32_e32 v31, v29
	v_pk_mul_f32 v[30:31], v[30:31], v[26:27] op_sel:[0,1] op_sel_hi:[1,0]
	v_add_u32_e32 v13, 0x16b00, v10
	v_pk_fma_f32 v[28:29], v[28:29], v[26:27], v[30:31] op_sel_hi:[0,1,1]
	ds_write_b64 v13, v[28:29]
	v_xor_b32_e32 v28, 0x80000000, v27
	v_mov_b32_e32 v29, v27
	v_pk_mul_f32 v[28:29], v[16:17], v[28:29] op_sel:[1,0] op_sel_hi:[0,1]
	v_pk_fma_f32 v[26:27], v[16:17], v[26:27], v[28:29] op_sel_hi:[1,0,1]
	v_xor_b32_e32 v28, 0x80000000, v53
	v_mov_b32_e32 v29, v53
	v_pk_mul_f32 v[28:29], v[28:29], v[26:27] op_sel:[0,1] op_sel_hi:[1,0]
	v_add_u32_e32 v13, 0x17b80, v10
	v_pk_fma_f32 v[28:29], v[52:53], v[26:27], v[28:29] op_sel_hi:[0,1,1]
	ds_write_b64 v13, v[28:29]
	v_xor_b32_e32 v28, 0x80000000, v27
	v_mov_b32_e32 v29, v27
	v_pk_mul_f32 v[28:29], v[16:17], v[28:29] op_sel:[1,0] op_sel_hi:[0,1]
	v_pk_fma_f32 v[26:27], v[16:17], v[26:27], v[28:29] op_sel_hi:[1,0,1]
	v_xor_b32_e32 v28, 0x80000000, v23
	v_mov_b32_e32 v29, v23
	v_pk_mul_f32 v[28:29], v[28:29], v[26:27] op_sel:[0,1] op_sel_hi:[1,0]
	v_add_u32_e32 v13, 0x18c00, v10
	v_pk_fma_f32 v[22:23], v[22:23], v[26:27], v[28:29] op_sel_hi:[0,1,1]
	ds_write_b64 v13, v[22:23]
	v_xor_b32_e32 v22, 0x80000000, v27
	v_mov_b32_e32 v23, v27
	v_pk_mul_f32 v[22:23], v[16:17], v[22:23] op_sel:[1,0] op_sel_hi:[0,1]
	v_pk_fma_f32 v[22:23], v[16:17], v[26:27], v[22:23] op_sel_hi:[1,0,1]
	v_xor_b32_e32 v26, 0x80000000, v39
	v_mov_b32_e32 v27, v39
	v_pk_mul_f32 v[26:27], v[26:27], v[22:23] op_sel:[0,1] op_sel_hi:[1,0]
	v_add_u32_e32 v13, 0x19c80, v10
	v_pk_fma_f32 v[26:27], v[38:39], v[22:23], v[26:27] op_sel_hi:[0,1,1]
	ds_write_b64 v13, v[26:27]
	v_xor_b32_e32 v26, 0x80000000, v23
	v_mov_b32_e32 v27, v23
	v_pk_mul_f32 v[26:27], v[16:17], v[26:27] op_sel:[1,0] op_sel_hi:[0,1]
	v_pk_fma_f32 v[22:23], v[16:17], v[22:23], v[26:27] op_sel_hi:[1,0,1]
	v_xor_b32_e32 v26, 0x80000000, v25
	v_mov_b32_e32 v27, v25
	v_pk_mul_f32 v[26:27], v[26:27], v[22:23] op_sel:[0,1] op_sel_hi:[1,0]
	v_add_u32_e32 v13, 0x1ad00, v10
	v_pk_fma_f32 v[24:25], v[24:25], v[22:23], v[26:27] op_sel_hi:[0,1,1]
	ds_write_b64 v13, v[24:25]
	v_xor_b32_e32 v24, 0x80000000, v23
	v_mov_b32_e32 v25, v23
	v_pk_mul_f32 v[24:25], v[16:17], v[24:25] op_sel:[1,0] op_sel_hi:[0,1]
	v_pk_fma_f32 v[22:23], v[16:17], v[22:23], v[24:25] op_sel_hi:[1,0,1]
	v_xor_b32_e32 v24, 0x80000000, v43
	v_mov_b32_e32 v25, v43
	v_pk_mul_f32 v[24:25], v[24:25], v[22:23] op_sel:[0,1] op_sel_hi:[1,0]
	v_add_u32_e32 v13, 0x1bd80, v10
	v_pk_fma_f32 v[24:25], v[42:43], v[22:23], v[24:25] op_sel_hi:[0,1,1]
	ds_write_b64 v13, v[24:25]
	v_xor_b32_e32 v24, 0x80000000, v23
	v_mov_b32_e32 v25, v23
	v_pk_mul_f32 v[24:25], v[16:17], v[24:25] op_sel:[1,0] op_sel_hi:[0,1]
	v_pk_fma_f32 v[22:23], v[16:17], v[22:23], v[24:25] op_sel_hi:[1,0,1]
	v_xor_b32_e32 v24, 0x80000000, v19
	v_mov_b32_e32 v25, v19
	v_pk_mul_f32 v[24:25], v[24:25], v[22:23] op_sel:[0,1] op_sel_hi:[1,0]
	v_add_u32_e32 v13, 0x1ce00, v10
	v_pk_fma_f32 v[18:19], v[18:19], v[22:23], v[24:25] op_sel_hi:[0,1,1]
	ds_write_b64 v13, v[18:19]
	v_xor_b32_e32 v18, 0x80000000, v23
	v_mov_b32_e32 v19, v23
	v_pk_mul_f32 v[18:19], v[16:17], v[18:19] op_sel:[1,0] op_sel_hi:[0,1]
	v_pk_fma_f32 v[18:19], v[16:17], v[22:23], v[18:19] op_sel_hi:[1,0,1]
	v_xor_b32_e32 v22, 0x80000000, v33
	v_mov_b32_e32 v23, v33
	v_pk_mul_f32 v[22:23], v[22:23], v[18:19] op_sel:[0,1] op_sel_hi:[1,0]
	v_add_u32_e32 v13, 0x1de80, v10
	v_pk_fma_f32 v[22:23], v[32:33], v[18:19], v[22:23] op_sel_hi:[0,1,1]
	ds_write_b64 v13, v[22:23]
	v_xor_b32_e32 v22, 0x80000000, v19
	v_mov_b32_e32 v23, v19
	v_pk_mul_f32 v[22:23], v[16:17], v[22:23] op_sel:[1,0] op_sel_hi:[0,1]
	v_pk_fma_f32 v[18:19], v[16:17], v[18:19], v[22:23] op_sel_hi:[1,0,1]
	v_xor_b32_e32 v22, 0x80000000, v21
	v_mov_b32_e32 v23, v21
	v_pk_mul_f32 v[22:23], v[22:23], v[18:19] op_sel:[0,1] op_sel_hi:[1,0]
	v_add_u32_e32 v13, 0x1ef00, v10
	v_pk_fma_f32 v[20:21], v[20:21], v[18:19], v[22:23] op_sel_hi:[0,1,1]
	ds_write_b64 v13, v[20:21]
	v_xor_b32_e32 v20, 0x80000000, v19
	v_mov_b32_e32 v21, v19
	v_pk_mul_f32 v[20:21], v[16:17], v[20:21] op_sel:[1,0] op_sel_hi:[0,1]
	v_pk_fma_f32 v[16:17], v[16:17], v[18:19], v[20:21] op_sel_hi:[1,0,1]
	v_xor_b32_e32 v18, 0x80000000, v37
	v_mov_b32_e32 v19, v37
	v_pk_mul_f32 v[18:19], v[18:19], v[16:17] op_sel:[0,1] op_sel_hi:[1,0]
	v_add_u32_e32 v10, 0x1ff80, v10
	v_pk_fma_f32 v[16:17], v[36:37], v[16:17], v[18:19] op_sel_hi:[0,1,1]
	ds_write_b64 v10, v[16:17]
	v_mov_b32_e32 v10, v174
	v_mov_b32_e32 v13, v172
	s_waitcnt lgkmcnt(0)
	s_barrier
	v_mov_b32_e32 v16, v180
	v_add_u32_e32 v15, v13, v10
	v_lshl_add_u32 v75, v15, 3, 0
	v_xad_u32 v15, v13, 1, v10
	v_lshl_add_u32 v74, v15, 3, 0
	v_xad_u32 v15, v13, 2, v10
	v_lshl_add_u32 v73, v15, 3, 0
	v_xad_u32 v15, v13, 3, v10
	v_lshl_add_u32 v72, v15, 3, 0
	v_xad_u32 v15, v13, 4, v10
	v_lshl_add_u32 v71, v15, 3, 0
	v_xad_u32 v15, v13, 5, v10
	v_lshl_add_u32 v70, v15, 3, 0
	v_xad_u32 v15, v13, 6, v10
	v_lshl_add_u32 v69, v15, 3, 0
	v_xad_u32 v15, v13, 7, v10
	v_lshl_add_u32 v68, v15, 3, 0
	v_xad_u32 v15, v13, 8, v10
	v_lshl_add_u32 v15, v15, 3, 0
	v_add_u32_e32 v67, 0x800, v15
	v_xad_u32 v15, v13, 9, v10
	v_lshl_add_u32 v15, v15, 3, 0
	v_add_u32_e32 v66, 0x800, v15
	v_xad_u32 v15, v13, 10, v10
	v_lshl_add_u32 v15, v15, 3, 0
	v_add_u32_e32 v65, 0x800, v15
	v_xad_u32 v15, v13, 11, v10
	v_lshl_add_u32 v15, v15, 3, 0
	v_add_u32_e32 v64, 0x800, v15
	v_xad_u32 v15, v13, 12, v10
	v_mov_b32_e32 v17, v181
	v_lshl_add_u32 v15, v15, 3, 0
	ds_read2_b64 v[18:21], v75 offset1:16
	ds_read2_b64 v[40:43], v67 offset1:16
	v_add_u32_e32 v63, 0x800, v15
	v_xad_u32 v15, v13, 13, v10
	v_lshl_add_u32 v15, v15, 3, 0
	v_add_u32_e32 v62, 0x800, v15
	v_xad_u32 v15, v13, 14, v10
	v_xad_u32 v10, v13, 15, v10
	ds_read2_b64 v[22:25], v74 offset0:32 offset1:48
	ds_read2_b64 v[48:51], v66 offset0:32 offset1:48
	v_lshl_add_u32 v15, v15, 3, 0
	v_lshl_add_u32 v10, v10, 3, 0
	v_add_u32_e32 v15, 0x800, v15
	v_add_u32_e32 v13, 0x800, v10
	v_mov_b32_e32 v10, v1
	ds_read2_b64 v[26:29], v73 offset0:64 offset1:80
	ds_read2_b64 v[58:61], v72 offset0:96 offset1:112
	ds_read2_b64 v[76:79], v71 offset0:128 offset1:144
	ds_read2_b64 v[80:83], v70 offset0:160 offset1:176
	ds_read2_b64 v[84:87], v69 offset0:192 offset1:208
	ds_read2_b64 v[88:91], v68 offset0:224 offset1:240
	ds_read2_b64 v[54:57], v65 offset0:64 offset1:80
	ds_read2_b64 v[92:95], v64 offset0:96 offset1:112
	ds_read2_b64 v[96:99], v63 offset0:128 offset1:144
	ds_read2_b64 v[100:103], v62 offset0:160 offset1:176
	ds_read2_b64 v[104:107], v15 offset0:192 offset1:208
	ds_read2_b64 v[108:111], v13 offset0:224 offset1:240
	s_waitcnt lgkmcnt(14)
	v_pk_add_f32 v[112:113], v[18:19], v[40:41]
	v_pk_add_f32 v[40:41], v[18:19], v[40:41] neg_lo:[0,1] neg_hi:[0,1]
	v_pk_add_f32 v[18:19], v[20:21], v[42:43]
	v_pk_add_f32 v[20:21], v[20:21], v[42:43] neg_lo:[0,1] neg_hi:[0,1]
	v_mov_b32_e32 v30, v164
	v_mov_b32_e32 v32, v165
	v_mov_b32_e32 v34, v166
	v_mov_b32_e32 v10, v167
	v_mov_b32_e32 v38, v168
	v_mov_b32_e32 v36, v169
	v_mov_b32_e32 v46, v170
	v_xor_b32_e32 v42, 0x80000000, v21
	v_mov_b32_e32 v43, v20
	v_mov_b32_e32 v31, v171
	v_pk_mul_f32 v[42:43], v[42:43], v[46:47] op_sel_hi:[1,0] neg_lo:[0,1] neg_hi:[0,1]
	s_nop 0
	v_pk_fma_f32 v[44:45], v[20:21], v[30:31], v[42:43] op_sel_hi:[1,0,1]
	s_waitcnt lgkmcnt(12)
	v_pk_add_f32 v[20:21], v[22:23], v[48:49]
	v_pk_add_f32 v[22:23], v[22:23], v[48:49] neg_lo:[0,1] neg_hi:[0,1]
	s_nop 0
	v_xor_b32_e32 v42, 0x80000000, v23
	v_mov_b32_e32 v43, v22
	v_pk_mul_f32 v[42:43], v[42:43], v[36:37] op_sel_hi:[1,0] neg_lo:[0,1] neg_hi:[0,1]
	s_nop 0
	v_pk_fma_f32 v[48:49], v[22:23], v[32:33], v[42:43] op_sel_hi:[1,0,1]
	v_pk_add_f32 v[22:23], v[24:25], v[50:51]
	v_pk_add_f32 v[24:25], v[24:25], v[50:51] neg_lo:[0,1] neg_hi:[0,1]
	s_nop 0
	v_xor_b32_e32 v42, 0x80000000, v25
	v_mov_b32_e32 v43, v24
	v_pk_mul_f32 v[42:43], v[42:43], v[38:39] op_sel_hi:[1,0] neg_lo:[0,1] neg_hi:[0,1]
	s_nop 0
	v_pk_fma_f32 v[52:53], v[24:25], v[34:35], v[42:43] op_sel_hi:[1,0,1]
	s_waitcnt lgkmcnt(5)
	v_pk_add_f32 v[24:25], v[26:27], v[54:55]
	v_pk_add_f32 v[26:27], v[26:27], v[54:55] neg_lo:[0,1] neg_hi:[0,1]
	s_nop 0
	v_xor_b32_e32 v42, 0x80000000, v27
	v_mov_b32_e32 v43, v26
	v_pk_mul_f32 v[42:43], v[42:43], v[10:11] op_sel_hi:[1,0] neg_lo:[0,1] neg_hi:[0,1]
	s_nop 0
	v_pk_fma_f32 v[54:55], v[26:27], v[10:11], v[42:43] op_sel_hi:[1,0,1]
	v_pk_add_f32 v[26:27], v[28:29], v[56:57]
	v_pk_add_f32 v[28:29], v[28:29], v[56:57] neg_lo:[0,1] neg_hi:[0,1]
	s_nop 0
	v_pk_mul_f32 v[42:43], v[28:29], v[38:39] op_sel_hi:[1,0]
	v_xor_b32_e32 v50, 0x80000000, v29
	v_mov_b32_e32 v51, v28
	v_pk_fma_f32 v[56:57], v[50:51], v[34:35], v[42:43] op_sel_hi:[1,0,1] neg_lo:[0,1,0] neg_hi:[0,1,0]
	s_waitcnt lgkmcnt(4)
	v_pk_add_f32 v[42:43], v[58:59], v[92:93] neg_lo:[0,1] neg_hi:[0,1]
	v_pk_add_f32 v[28:29], v[58:59], v[92:93]
	v_pk_mul_f32 v[50:51], v[42:43], v[36:37] op_sel_hi:[1,0]
	v_xor_b32_e32 v58, 0x80000000, v43
	v_mov_b32_e32 v59, v42
	v_pk_fma_f32 v[58:59], v[58:59], v[32:33], v[50:51] op_sel_hi:[1,0,1] neg_lo:[0,1,0] neg_hi:[0,1,0]
	v_pk_add_f32 v[50:51], v[60:61], v[94:95] neg_lo:[0,1] neg_hi:[0,1]
	v_pk_add_f32 v[42:43], v[60:61], v[94:95]
	v_pk_mul_f32 v[60:61], v[50:51], v[46:47] op_sel_hi:[1,0]
	v_xor_b32_e32 v92, 0x80000000, v51
	v_mov_b32_e32 v93, v50
	s_waitcnt lgkmcnt(3)
	v_pk_add_f32 v[50:51], v[76:77], v[96:97]
	v_pk_add_f32 v[76:77], v[76:77], v[96:97] neg_lo:[0,1] neg_hi:[0,1]
	v_pk_fma_f32 v[60:61], v[92:93], v[30:31], v[60:61] op_sel_hi:[1,0,1] neg_lo:[0,1,0] neg_hi:[0,1,0]
	v_xor_b32_e32 v93, 0x80000000, v76
	v_mov_b32_e32 v92, v77
	v_pk_add_f32 v[76:77], v[78:79], v[98:99]
	v_pk_add_f32 v[78:79], v[78:79], v[98:99] neg_lo:[0,1] neg_hi:[0,1]
	s_nop 0
	v_pk_mul_f32 v[94:95], v[78:79], v[46:47] op_sel_hi:[1,0] neg_lo:[0,1] neg_hi:[0,1]
	v_xor_b32_e32 v96, 0x80000000, v79
	v_mov_b32_e32 v97, v78
	v_pk_fma_f32 v[78:79], v[96:97], v[30:31], v[94:95] op_sel_hi:[1,0,1] neg_lo:[0,1,0] neg_hi:[0,1,0]
	s_waitcnt lgkmcnt(2)
	v_pk_add_f32 v[94:95], v[80:81], v[100:101]
	v_pk_add_f32 v[80:81], v[80:81], v[100:101] neg_lo:[0,1] neg_hi:[0,1]
	s_nop 0
	v_pk_mul_f32 v[96:97], v[80:81], v[36:37] op_sel_hi:[1,0] neg_lo:[0,1] neg_hi:[0,1]
	v_xor_b32_e32 v98, 0x80000000, v81
	v_mov_b32_e32 v99, v80
	v_pk_fma_f32 v[80:81], v[98:99], v[32:33], v[96:97] op_sel_hi:[1,0,1] neg_lo:[0,1,0] neg_hi:[0,1,0]
	v_pk_add_f32 v[96:97], v[82:83], v[102:103]
	v_pk_add_f32 v[82:83], v[82:83], v[102:103] neg_lo:[0,1] neg_hi:[0,1]
	s_nop 0
	v_pk_mul_f32 v[98:99], v[82:83], v[38:39] op_sel_hi:[1,0] neg_lo:[0,1] neg_hi:[0,1]
	v_xor_b32_e32 v100, 0x80000000, v83
	v_mov_b32_e32 v101, v82
	v_pk_fma_f32 v[82:83], v[100:101], v[34:35], v[98:99] op_sel_hi:[1,0,1] neg_lo:[0,1,0] neg_hi:[0,1,0]
	s_waitcnt lgkmcnt(1)
	v_pk_add_f32 v[98:99], v[84:85], v[104:105]
	v_pk_add_f32 v[84:85], v[84:85], v[104:105] neg_lo:[0,1] neg_hi:[0,1]
	s_nop 0
	v_xor_b32_e32 v100, 0x80000000, v85
	v_mov_b32_e32 v101, v84
	v_pk_mul_f32 v[100:101], v[100:101], v[10:11] op_sel_hi:[1,0] neg_lo:[0,1] neg_hi:[0,1]
	s_nop 0
	v_pk_fma_f32 v[84:85], v[84:85], v[10:11], v[100:101] op_sel_hi:[1,0,1] neg_lo:[0,1,0] neg_hi:[0,1,0]
	v_pk_add_f32 v[100:101], v[86:87], v[106:107]
	v_pk_add_f32 v[86:87], v[86:87], v[106:107] neg_lo:[0,1] neg_hi:[0,1]
	s_nop 0
	v_xor_b32_e32 v102, 0x80000000, v87
	v_mov_b32_e32 v103, v86
	v_pk_mul_f32 v[38:39], v[102:103], v[38:39] op_sel_hi:[1,0] neg_lo:[0,1] neg_hi:[0,1]
	s_nop 0
	v_pk_fma_f32 v[86:87], v[86:87], v[34:35], v[38:39] op_sel_hi:[1,0,1] neg_lo:[0,1,0] neg_hi:[0,1,0]
	s_waitcnt lgkmcnt(0)
	v_pk_add_f32 v[38:39], v[88:89], v[108:109] neg_lo:[0,1] neg_hi:[0,1]
	v_pk_add_f32 v[34:35], v[88:89], v[108:109]
	v_xor_b32_e32 v88, 0x80000000, v39
	v_mov_b32_e32 v89, v38
	v_pk_mul_f32 v[88:89], v[88:89], v[36:37] op_sel_hi:[1,0] neg_lo:[0,1] neg_hi:[0,1]
	s_nop 0
	v_pk_fma_f32 v[88:89], v[38:39], v[32:33], v[88:89] op_sel_hi:[1,0,1] neg_lo:[0,1,0] neg_hi:[0,1,0]
	v_pk_add_f32 v[38:39], v[90:91], v[110:111]
	v_pk_add_f32 v[90:91], v[90:91], v[110:111] neg_lo:[0,1] neg_hi:[0,1]
	s_nop 0
	v_xor_b32_e32 v102, 0x80000000, v91
	v_mov_b32_e32 v103, v90
	v_pk_mul_f32 v[46:47], v[102:103], v[46:47] op_sel_hi:[1,0] neg_lo:[0,1] neg_hi:[0,1]
	s_nop 0
	v_pk_fma_f32 v[90:91], v[90:91], v[30:31], v[46:47] op_sel_hi:[1,0,1] neg_lo:[0,1,0] neg_hi:[0,1,0]
	v_pk_add_f32 v[46:47], v[18:19], v[76:77]
	v_pk_add_f32 v[18:19], v[18:19], v[76:77] neg_lo:[0,1] neg_hi:[0,1]
	v_pk_add_f32 v[30:31], v[112:113], v[50:51]
	v_xor_b32_e32 v76, 0x80000000, v19
	v_mov_b32_e32 v77, v18
	v_pk_mul_f32 v[76:77], v[76:77], v[36:37] op_sel_hi:[1,0] neg_lo:[0,1] neg_hi:[0,1]
	v_pk_add_f32 v[50:51], v[112:113], v[50:51] neg_lo:[0,1] neg_hi:[0,1]
	v_pk_fma_f32 v[76:77], v[18:19], v[32:33], v[76:77] op_sel_hi:[1,0,1]
	v_pk_add_f32 v[18:19], v[20:21], v[94:95]
	v_pk_add_f32 v[20:21], v[20:21], v[94:95] neg_lo:[0,1] neg_hi:[0,1]
	s_nop 0
	v_xor_b32_e32 v94, 0x80000000, v21
	v_mov_b32_e32 v95, v20
	v_pk_mul_f32 v[94:95], v[94:95], v[10:11] op_sel_hi:[1,0] neg_lo:[0,1] neg_hi:[0,1]
	s_nop 0
	v_pk_fma_f32 v[20:21], v[20:21], v[10:11], v[94:95] op_sel_hi:[1,0,1]
	v_pk_add_f32 v[94:95], v[22:23], v[96:97]
	v_pk_add_f32 v[22:23], v[22:23], v[96:97] neg_lo:[0,1] neg_hi:[0,1]
	s_nop 0
	v_pk_mul_f32 v[96:97], v[22:23], v[36:37] op_sel_hi:[1,0]
	v_xor_b32_e32 v102, 0x80000000, v23
	v_mov_b32_e32 v103, v22
	v_pk_add_f32 v[22:23], v[24:25], v[98:99]
	v_pk_add_f32 v[24:25], v[24:25], v[98:99] neg_lo:[0,1] neg_hi:[0,1]
	v_pk_fma_f32 v[96:97], v[102:103], v[32:33], v[96:97] op_sel_hi:[1,0,1] neg_lo:[0,1,0] neg_hi:[0,1,0]
	v_xor_b32_e32 v99, 0x80000000, v24
	v_mov_b32_e32 v98, v25
	v_pk_add_f32 v[24:25], v[26:27], v[100:101]
	v_pk_add_f32 v[26:27], v[26:27], v[100:101] neg_lo:[0,1] neg_hi:[0,1]
	s_nop 0
	v_pk_mul_f32 v[100:101], v[26:27], v[36:37] op_sel_hi:[1,0] neg_lo:[0,1] neg_hi:[0,1]
	v_xor_b32_e32 v102, 0x80000000, v27
	v_mov_b32_e32 v103, v26
	v_pk_add_f32 v[26:27], v[28:29], v[34:35]
	v_pk_add_f32 v[28:29], v[28:29], v[34:35] neg_lo:[0,1] neg_hi:[0,1]
	v_pk_fma_f32 v[100:101], v[102:103], v[32:33], v[100:101] op_sel_hi:[1,0,1] neg_lo:[0,1,0] neg_hi:[0,1,0]
	v_xor_b32_e32 v34, 0x80000000, v29
	v_mov_b32_e32 v35, v28
	v_pk_mul_f32 v[34:35], v[34:35], v[10:11] op_sel_hi:[1,0] neg_lo:[0,1] neg_hi:[0,1]
	v_pk_add_f32 v[102:103], v[30:31], v[22:23] neg_lo:[0,1] neg_hi:[0,1]
	v_pk_fma_f32 v[28:29], v[28:29], v[10:11], v[34:35] op_sel_hi:[1,0,1] neg_lo:[0,1,0] neg_hi:[0,1,0]
	v_pk_add_f32 v[34:35], v[42:43], v[38:39]
	v_pk_add_f32 v[38:39], v[42:43], v[38:39] neg_lo:[0,1] neg_hi:[0,1]
	s_nop 0
	v_xor_b32_e32 v42, 0x80000000, v39
	v_mov_b32_e32 v43, v38
	v_pk_mul_f32 v[42:43], v[42:43], v[36:37] op_sel_hi:[1,0] neg_lo:[0,1] neg_hi:[0,1]
	s_nop 0
	v_pk_fma_f32 v[42:43], v[38:39], v[32:33], v[42:43] op_sel_hi:[1,0,1] neg_lo:[0,1,0] neg_hi:[0,1,0]
	v_pk_add_f32 v[38:39], v[30:31], v[22:23]
	v_pk_add_f32 v[22:23], v[46:47], v[24:25]
	v_pk_add_f32 v[24:25], v[46:47], v[24:25] neg_lo:[0,1] neg_hi:[0,1]
	s_nop 0
	v_xor_b32_e32 v30, 0x80000000, v25
	v_mov_b32_e32 v31, v24
	v_pk_mul_f32 v[30:31], v[30:31], v[10:11] op_sel_hi:[1,0] neg_lo:[0,1] neg_hi:[0,1]
	s_nop 0
	v_pk_fma_f32 v[24:25], v[24:25], v[10:11], v[30:31] op_sel_hi:[1,0,1]
	v_pk_add_f32 v[30:31], v[18:19], v[26:27]
	v_pk_add_f32 v[18:19], v[18:19], v[26:27] neg_lo:[0,1] neg_hi:[0,1]
	s_nop 0
	v_xor_b32_e32 v27, 0x80000000, v18
	v_mov_b32_e32 v26, v19
	v_pk_add_f32 v[18:19], v[94:95], v[34:35]
	v_pk_add_f32 v[34:35], v[94:95], v[34:35] neg_lo:[0,1] neg_hi:[0,1]
	s_nop 0
	v_xor_b32_e32 v46, 0x80000000, v35
	v_mov_b32_e32 v47, v34
	v_pk_mul_f32 v[46:47], v[46:47], v[10:11] op_sel_hi:[1,0] neg_lo:[0,1] neg_hi:[0,1]
	s_nop 0
	v_pk_fma_f32 v[34:35], v[34:35], v[10:11], v[46:47] op_sel_hi:[1,0,1] neg_lo:[0,1,0] neg_hi:[0,1,0]
	v_pk_add_f32 v[46:47], v[38:39], v[30:31]
	v_pk_add_f32 v[38:39], v[38:39], v[30:31] neg_lo:[0,1] neg_hi:[0,1]
	v_pk_add_f32 v[30:31], v[22:23], v[18:19]
	v_pk_add_f32 v[18:19], v[22:23], v[18:19] neg_lo:[0,1] neg_hi:[0,1]
	v_pk_add_f32 v[94:95], v[46:47], v[30:31]
	v_xor_b32_e32 v23, 0x80000000, v18
	v_mov_b32_e32 v22, v19
	v_pk_add_f32 v[18:19], v[102:103], v[26:27]
	v_pk_add_f32 v[102:103], v[102:103], v[26:27] neg_lo:[0,1] neg_hi:[0,1]
	v_pk_add_f32 v[26:27], v[24:25], v[34:35]
	v_pk_add_f32 v[24:25], v[24:25], v[34:35] neg_lo:[0,1] neg_hi:[0,1]
	v_pk_add_f32 v[30:31], v[46:47], v[30:31] neg_lo:[0,1] neg_hi:[0,1]
	v_xor_b32_e32 v35, 0x80000000, v24
	v_mov_b32_e32 v34, v25
	v_pk_add_f32 v[24:25], v[50:51], v[98:99]
	v_pk_add_f32 v[98:99], v[50:51], v[98:99] neg_lo:[0,1] neg_hi:[0,1]
	v_pk_add_f32 v[50:51], v[76:77], v[100:101] neg_lo:[0,1] neg_hi:[0,1]
	v_pk_add_f32 v[46:47], v[38:39], v[22:23]
	v_pk_add_f32 v[22:23], v[38:39], v[22:23] neg_lo:[0,1] neg_hi:[0,1]
	v_pk_add_f32 v[104:105], v[18:19], v[26:27]
	v_pk_add_f32 v[26:27], v[18:19], v[26:27] neg_lo:[0,1] neg_hi:[0,1]
	v_pk_add_f32 v[38:39], v[102:103], v[34:35]
	v_pk_add_f32 v[18:19], v[102:103], v[34:35] neg_lo:[0,1] neg_hi:[0,1]
	v_pk_add_f32 v[34:35], v[76:77], v[100:101]
	v_xor_b32_e32 v76, 0x80000000, v51
	v_mov_b32_e32 v77, v50
	v_pk_mul_f32 v[76:77], v[10:11], v[76:77] op_sel_hi:[0,1] neg_lo:[1,0] neg_hi:[1,0]
	v_pk_fma_f32 v[76:77], v[10:11], v[50:51], v[76:77] op_sel_hi:[0,1,1]
	v_pk_add_f32 v[50:51], v[20:21], v[28:29]
	v_pk_add_f32 v[20:21], v[20:21], v[28:29] neg_lo:[0,1] neg_hi:[0,1]
	s_nop 0
	v_xor_b32_e32 v29, 0x80000000, v20
	v_mov_b32_e32 v28, v21
	v_pk_add_f32 v[20:21], v[96:97], v[42:43]
	v_pk_add_f32 v[42:43], v[96:97], v[42:43] neg_lo:[0,1] neg_hi:[0,1]
	s_nop 0
	v_xor_b32_e32 v96, 0x80000000, v43
	v_mov_b32_e32 v97, v42
	v_pk_mul_f32 v[96:97], v[10:11], v[96:97] op_sel_hi:[0,1] neg_lo:[1,0] neg_hi:[1,0]
	v_pk_fma_f32 v[42:43], v[10:11], v[42:43], v[96:97] op_sel_hi:[0,1,1] neg_lo:[1,0,0] neg_hi:[1,0,0]
	v_pk_add_f32 v[96:97], v[24:25], v[50:51]
	v_pk_add_f32 v[24:25], v[24:25], v[50:51] neg_lo:[0,1] neg_hi:[0,1]
	v_pk_add_f32 v[50:51], v[34:35], v[20:21]
	v_pk_add_f32 v[20:21], v[34:35], v[20:21] neg_lo:[0,1] neg_hi:[0,1]
	v_pk_add_f32 v[102:103], v[96:97], v[50:51]
	v_xor_b32_e32 v101, 0x80000000, v20
	v_mov_b32_e32 v100, v21
	v_pk_add_f32 v[34:35], v[96:97], v[50:51] neg_lo:[0,1] neg_hi:[0,1]
	v_pk_add_f32 v[20:21], v[98:99], v[28:29]
	v_pk_add_f32 v[96:97], v[98:99], v[28:29] neg_lo:[0,1] neg_hi:[0,1]
	v_pk_add_f32 v[28:29], v[76:77], v[42:43]
	v_pk_add_f32 v[42:43], v[76:77], v[42:43] neg_lo:[0,1] neg_hi:[0,1]
	v_pk_add_f32 v[98:99], v[20:21], v[28:29]
	v_xor_b32_e32 v77, 0x80000000, v42
	v_mov_b32_e32 v76, v43
	v_pk_add_f32 v[28:29], v[20:21], v[28:29] neg_lo:[0,1] neg_hi:[0,1]
	v_pk_add_f32 v[42:43], v[96:97], v[76:77]
	v_pk_add_f32 v[20:21], v[96:97], v[76:77] neg_lo:[0,1] neg_hi:[0,1]
	v_pk_add_f32 v[76:77], v[40:41], v[92:93]
	v_pk_add_f32 v[92:93], v[40:41], v[92:93] neg_lo:[0,1] neg_hi:[0,1]
	v_pk_add_f32 v[40:41], v[44:45], v[78:79]
	v_pk_add_f32 v[44:45], v[44:45], v[78:79] neg_lo:[0,1] neg_hi:[0,1]
	v_pk_add_f32 v[50:51], v[24:25], v[100:101]
	v_xor_b32_e32 v78, 0x80000000, v45
	v_mov_b32_e32 v79, v44
	v_pk_mul_f32 v[78:79], v[36:37], v[78:79] op_sel_hi:[0,1] neg_lo:[1,0] neg_hi:[1,0]
	v_pk_fma_f32 v[44:45], v[32:33], v[44:45], v[78:79] op_sel_hi:[0,1,1]
	v_pk_add_f32 v[78:79], v[48:49], v[80:81]
	v_pk_add_f32 v[48:49], v[48:49], v[80:81] neg_lo:[0,1] neg_hi:[0,1]
	v_pk_add_f32 v[24:25], v[24:25], v[100:101] neg_lo:[0,1] neg_hi:[0,1]
	v_xor_b32_e32 v80, 0x80000000, v49
	v_mov_b32_e32 v81, v48
	v_pk_mul_f32 v[80:81], v[10:11], v[80:81] op_sel_hi:[0,1] neg_lo:[1,0] neg_hi:[1,0]
	v_pk_fma_f32 v[80:81], v[10:11], v[48:49], v[80:81] op_sel_hi:[0,1,1]
	v_pk_add_f32 v[48:49], v[52:53], v[82:83]
	v_pk_add_f32 v[52:53], v[52:53], v[82:83] neg_lo:[0,1] neg_hi:[0,1]
	s_nop 0
	v_xor_b32_e32 v82, 0x80000000, v53
	v_mov_b32_e32 v83, v52
	v_pk_mul_f32 v[82:83], v[32:33], v[82:83] op_sel_hi:[0,1] neg_lo:[1,0] neg_hi:[1,0]
	v_pk_fma_f32 v[52:53], v[36:37], v[52:53], v[82:83] op_sel_hi:[0,1,1]
	v_pk_add_f32 v[82:83], v[54:55], v[84:85]
	v_pk_add_f32 v[54:55], v[54:55], v[84:85] neg_lo:[0,1] neg_hi:[0,1]
	s_nop 0
	v_xor_b32_e32 v85, 0x80000000, v54
	v_mov_b32_e32 v84, v55
	v_pk_add_f32 v[54:55], v[56:57], v[86:87]
	v_pk_add_f32 v[56:57], v[56:57], v[86:87] neg_lo:[0,1] neg_hi:[0,1]
	s_nop 0
	v_xor_b32_e32 v86, 0x80000000, v57
	v_mov_b32_e32 v87, v56
	v_pk_mul_f32 v[86:87], v[32:33], v[86:87] op_sel_hi:[0,1] neg_lo:[1,0] neg_hi:[1,0]
	v_pk_fma_f32 v[56:57], v[36:37], v[56:57], v[86:87] op_sel_hi:[0,1,1] neg_lo:[1,0,0] neg_hi:[1,0,0]
	v_pk_add_f32 v[86:87], v[58:59], v[88:89]
	v_pk_add_f32 v[58:59], v[58:59], v[88:89] neg_lo:[0,1] neg_hi:[0,1]
	s_nop 0
	v_xor_b32_e32 v88, 0x80000000, v59
	v_mov_b32_e32 v89, v58
	v_pk_mul_f32 v[88:89], v[10:11], v[88:89] op_sel_hi:[0,1] neg_lo:[1,0] neg_hi:[1,0]
	v_pk_fma_f32 v[58:59], v[10:11], v[58:59], v[88:89] op_sel_hi:[0,1,1] neg_lo:[1,0,0] neg_hi:[1,0,0]
	v_pk_add_f32 v[88:89], v[60:61], v[90:91]
	v_pk_add_f32 v[60:61], v[60:61], v[90:91] neg_lo:[0,1] neg_hi:[0,1]
	s_nop 0
	v_xor_b32_e32 v90, 0x80000000, v61
	v_mov_b32_e32 v91, v60
	v_pk_mul_f32 v[36:37], v[36:37], v[90:91] op_sel_hi:[0,1] neg_lo:[1,0] neg_hi:[1,0]
	v_pk_fma_f32 v[36:37], v[32:33], v[60:61], v[36:37] op_sel_hi:[0,1,1] neg_lo:[1,0,0] neg_hi:[1,0,0]
	v_pk_add_f32 v[32:33], v[76:77], v[82:83]
	v_pk_add_f32 v[60:61], v[76:77], v[82:83] neg_lo:[0,1] neg_hi:[0,1]
	v_pk_add_f32 v[76:77], v[54:55], v[40:41]
	v_pk_add_f32 v[40:41], v[40:41], v[54:55] neg_lo:[0,1] neg_hi:[0,1]
	s_nop 0
	v_xor_b32_e32 v54, 0x80000000, v41
	v_mov_b32_e32 v55, v40
	v_pk_mul_f32 v[54:55], v[10:11], v[54:55] op_sel_hi:[0,1] neg_lo:[1,0] neg_hi:[1,0]
	v_pk_fma_f32 v[54:55], v[10:11], v[40:41], v[54:55] op_sel_hi:[0,1,1]
	v_pk_add_f32 v[40:41], v[78:79], v[86:87]
	v_pk_add_f32 v[78:79], v[78:79], v[86:87] neg_lo:[0,1] neg_hi:[0,1]
	s_nop 0
	v_xor_b32_e32 v83, 0x80000000, v78
	v_mov_b32_e32 v82, v79
	v_pk_add_f32 v[78:79], v[48:49], v[88:89]
	v_pk_add_f32 v[48:49], v[48:49], v[88:89] neg_lo:[0,1] neg_hi:[0,1]
	v_pk_add_f32 v[88:89], v[76:77], v[78:79]
	v_xor_b32_e32 v86, 0x80000000, v49
	v_mov_b32_e32 v87, v48
	v_pk_mul_f32 v[86:87], v[10:11], v[86:87] op_sel_hi:[0,1] neg_lo:[1,0] neg_hi:[1,0]
	v_pk_fma_f32 v[48:49], v[10:11], v[48:49], v[86:87] op_sel_hi:[0,1,1] neg_lo:[1,0,0] neg_hi:[1,0,0]
	v_pk_add_f32 v[86:87], v[32:33], v[40:41]
	v_pk_add_f32 v[32:33], v[32:33], v[40:41] neg_lo:[0,1] neg_hi:[0,1]
	v_pk_add_f32 v[40:41], v[76:77], v[78:79] neg_lo:[0,1] neg_hi:[0,1]
	v_pk_add_f32 v[78:79], v[86:87], v[88:89] neg_lo:[0,1] neg_hi:[0,1]
	v_xor_b32_e32 v77, 0x80000000, v40
	v_mov_b32_e32 v76, v41
	v_pk_add_f32 v[90:91], v[32:33], v[76:77]
	v_pk_add_f32 v[40:41], v[32:33], v[76:77] neg_lo:[0,1] neg_hi:[0,1]
	v_pk_add_f32 v[76:77], v[54:55], v[48:49]
	v_pk_add_f32 v[48:49], v[54:55], v[48:49] neg_lo:[0,1] neg_hi:[0,1]
	v_pk_add_f32 v[32:33], v[60:61], v[82:83]
	v_pk_add_f32 v[60:61], v[60:61], v[82:83] neg_lo:[0,1] neg_hi:[0,1]
	v_xor_b32_e32 v55, 0x80000000, v48
	v_mov_b32_e32 v54, v49
	v_pk_add_f32 v[82:83], v[32:33], v[76:77]
	v_pk_add_f32 v[48:49], v[32:33], v[76:77] neg_lo:[0,1] neg_hi:[0,1]
	v_pk_add_f32 v[76:77], v[60:61], v[54:55]
	v_pk_add_f32 v[32:33], v[60:61], v[54:55] neg_lo:[0,1] neg_hi:[0,1]
	v_pk_add_f32 v[54:55], v[92:93], v[84:85]
	v_pk_add_f32 v[60:61], v[92:93], v[84:85] neg_lo:[0,1] neg_hi:[0,1]
	v_pk_add_f32 v[84:85], v[56:57], v[44:45]
	v_pk_add_f32 v[44:45], v[44:45], v[56:57] neg_lo:[0,1] neg_hi:[0,1]
	v_pk_add_f32 v[86:87], v[86:87], v[88:89]
	v_xor_b32_e32 v56, 0x80000000, v45
	v_mov_b32_e32 v57, v44
	v_pk_mul_f32 v[56:57], v[10:11], v[56:57] op_sel_hi:[0,1] neg_lo:[1,0] neg_hi:[1,0]
	v_pk_fma_f32 v[56:57], v[10:11], v[44:45], v[56:57] op_sel_hi:[0,1,1]
	v_pk_add_f32 v[44:45], v[80:81], v[58:59]
	v_pk_add_f32 v[58:59], v[80:81], v[58:59] neg_lo:[0,1] neg_hi:[0,1]
	v_xor_b32_e32 v88, 0x80000000, v87
	v_xor_b32_e32 v81, 0x80000000, v58
	v_mov_b32_e32 v80, v59
	v_pk_add_f32 v[58:59], v[52:53], v[36:37]
	v_pk_add_f32 v[36:37], v[52:53], v[36:37] neg_lo:[0,1] neg_hi:[0,1]
	v_mov_b32_e32 v89, v87
	v_xor_b32_e32 v52, 0x80000000, v37
	v_mov_b32_e32 v53, v36
	v_pk_mul_f32 v[52:53], v[10:11], v[52:53] op_sel_hi:[0,1] neg_lo:[1,0] neg_hi:[1,0]
	v_pk_fma_f32 v[36:37], v[10:11], v[36:37], v[52:53] op_sel_hi:[0,1,1] neg_lo:[1,0,0] neg_hi:[1,0,0]
	v_pk_add_f32 v[52:53], v[54:55], v[44:45]
	v_pk_add_f32 v[44:45], v[54:55], v[44:45] neg_lo:[0,1] neg_hi:[0,1]
	v_pk_add_f32 v[54:55], v[84:85], v[58:59]
	v_pk_add_f32 v[58:59], v[84:85], v[58:59] neg_lo:[0,1] neg_hi:[0,1]
	s_nop 0
	v_xor_b32_e32 v85, 0x80000000, v58
	v_mov_b32_e32 v84, v59
	v_pk_add_f32 v[58:59], v[52:53], v[54:55]
	v_pk_add_f32 v[52:53], v[52:53], v[54:55] neg_lo:[0,1] neg_hi:[0,1]
	v_pk_add_f32 v[54:55], v[44:45], v[84:85]
	v_pk_add_f32 v[44:45], v[44:45], v[84:85] neg_lo:[0,1] neg_hi:[0,1]
	v_pk_add_f32 v[84:85], v[60:61], v[80:81]
	v_pk_add_f32 v[60:61], v[60:61], v[80:81] neg_lo:[0,1] neg_hi:[0,1]
	v_pk_add_f32 v[80:81], v[56:57], v[36:37]
	v_pk_add_f32 v[36:37], v[56:57], v[36:37] neg_lo:[0,1] neg_hi:[0,1]
	v_pk_add_f32 v[92:93], v[84:85], v[80:81]
	v_xor_b32_e32 v57, 0x80000000, v36
	v_mov_b32_e32 v56, v37
	v_pk_add_f32 v[80:81], v[84:85], v[80:81] neg_lo:[0,1] neg_hi:[0,1]
	v_pk_add_f32 v[84:85], v[60:61], v[56:57]
	v_pk_add_f32 v[36:37], v[60:61], v[56:57] neg_lo:[0,1] neg_hi:[0,1]
	v_xor_b32_e32 v56, 0x80000000, v95
	v_mov_b32_e32 v57, v95
	v_pk_fma_f32 v[60:61], v[16:17], s[90:91], v[16:17] op_sel:[1,0,0] op_sel_hi:[0,1,1]
	v_pk_mul_f32 v[56:57], v[56:57], s[14:15]
	v_pk_mul_f32 v[88:89], v[60:61], v[88:89] op_sel:[1,0] op_sel_hi:[0,1]
	v_pk_fma_f32 v[56:57], v[94:95], s[94:95], v[56:57] op_sel_hi:[0,1,1]
	v_pk_fma_f32 v[86:87], v[60:61], v[86:87], v[88:89] op_sel_hi:[1,0,1]
	ds_write2_b64 v75, v[56:57], v[86:87] offset1:16
	v_xor_b32_e32 v56, 0x80000000, v61
	v_mov_b32_e32 v57, v61
	v_pk_mul_f32 v[56:57], v[16:17], v[56:57] op_sel:[1,0] op_sel_hi:[0,1]
	v_pk_fma_f32 v[56:57], v[16:17], v[60:61], v[56:57] op_sel_hi:[1,0,1]
	v_xor_b32_e32 v60, 0x80000000, v103
	v_mov_b32_e32 v61, v103
	v_xor_b32_e32 v86, 0x80000000, v57
	v_mov_b32_e32 v87, v57
	v_pk_mul_f32 v[60:61], v[56:57], v[60:61] op_sel:[1,0] op_sel_hi:[0,1]
	v_pk_mul_f32 v[86:87], v[16:17], v[86:87] op_sel:[1,0] op_sel_hi:[0,1]
	v_pk_fma_f32 v[60:61], v[56:57], v[102:103], v[60:61] op_sel_hi:[1,0,1]
	v_pk_fma_f32 v[56:57], v[16:17], v[56:57], v[86:87] op_sel_hi:[1,0,1]
	v_xor_b32_e32 v86, 0x80000000, v59
	v_mov_b32_e32 v87, v59
	v_pk_mul_f32 v[86:87], v[56:57], v[86:87] op_sel:[1,0] op_sel_hi:[0,1]
	v_pk_fma_f32 v[58:59], v[56:57], v[58:59], v[86:87] op_sel_hi:[1,0,1]
	ds_write2_b64 v74, v[60:61], v[58:59] offset0:32 offset1:48
	v_xor_b32_e32 v58, 0x80000000, v57
	v_mov_b32_e32 v59, v57
	v_pk_mul_f32 v[58:59], v[16:17], v[58:59] op_sel:[1,0] op_sel_hi:[0,1]
	v_pk_fma_f32 v[56:57], v[16:17], v[56:57], v[58:59] op_sel_hi:[1,0,1]
	v_xor_b32_e32 v58, 0x80000000, v105
	v_mov_b32_e32 v59, v105
	v_xor_b32_e32 v60, 0x80000000, v57
	v_mov_b32_e32 v61, v57
	v_pk_mul_f32 v[58:59], v[56:57], v[58:59] op_sel:[1,0] op_sel_hi:[0,1]
	v_pk_mul_f32 v[60:61], v[16:17], v[60:61] op_sel:[1,0] op_sel_hi:[0,1]
	v_pk_fma_f32 v[58:59], v[56:57], v[104:105], v[58:59] op_sel_hi:[1,0,1]
	v_pk_fma_f32 v[56:57], v[16:17], v[56:57], v[60:61] op_sel_hi:[1,0,1]
	v_xor_b32_e32 v60, 0x80000000, v83
	v_mov_b32_e32 v61, v83
	v_pk_mul_f32 v[60:61], v[56:57], v[60:61] op_sel:[1,0] op_sel_hi:[0,1]
	v_pk_fma_f32 v[60:61], v[56:57], v[82:83], v[60:61] op_sel_hi:[1,0,1]
	ds_write2_b64 v73, v[58:59], v[60:61] offset0:64 offset1:80
	v_xor_b32_e32 v58, 0x80000000, v57
	v_mov_b32_e32 v59, v57
	v_pk_mul_f32 v[58:59], v[16:17], v[58:59] op_sel:[1,0] op_sel_hi:[0,1]
	v_pk_fma_f32 v[56:57], v[16:17], v[56:57], v[58:59] op_sel_hi:[1,0,1]
	v_xor_b32_e32 v58, 0x80000000, v99
	v_mov_b32_e32 v59, v99
	v_xor_b32_e32 v60, 0x80000000, v57
	v_mov_b32_e32 v61, v57
	v_pk_mul_f32 v[58:59], v[56:57], v[58:59] op_sel:[1,0] op_sel_hi:[0,1]
	v_pk_mul_f32 v[60:61], v[16:17], v[60:61] op_sel:[1,0] op_sel_hi:[0,1]
	v_pk_fma_f32 v[58:59], v[56:57], v[98:99], v[58:59] op_sel_hi:[1,0,1]
	v_pk_fma_f32 v[56:57], v[16:17], v[56:57], v[60:61] op_sel_hi:[1,0,1]
	v_xor_b32_e32 v60, 0x80000000, v93
	v_mov_b32_e32 v61, v93
	v_pk_mul_f32 v[60:61], v[56:57], v[60:61] op_sel:[1,0] op_sel_hi:[0,1]
	v_pk_fma_f32 v[60:61], v[56:57], v[92:93], v[60:61] op_sel_hi:[1,0,1]
	ds_write2_b64 v72, v[58:59], v[60:61] offset0:96 offset1:112
	v_xor_b32_e32 v58, 0x80000000, v57
	v_mov_b32_e32 v59, v57
	v_pk_mul_f32 v[58:59], v[16:17], v[58:59] op_sel:[1,0] op_sel_hi:[0,1]
	v_pk_fma_f32 v[56:57], v[16:17], v[56:57], v[58:59] op_sel_hi:[1,0,1]
	v_xor_b32_e32 v58, 0x80000000, v47
	v_mov_b32_e32 v59, v47
	v_pk_mul_f32 v[58:59], v[56:57], v[58:59] op_sel:[1,0] op_sel_hi:[0,1]
	v_pk_fma_f32 v[46:47], v[56:57], v[46:47], v[58:59] op_sel_hi:[1,0,1]
	v_xor_b32_e32 v58, 0x80000000, v57
	v_mov_b32_e32 v59, v57
	v_pk_mul_f32 v[58:59], v[16:17], v[58:59] op_sel:[1,0] op_sel_hi:[0,1]
	v_pk_fma_f32 v[56:57], v[16:17], v[56:57], v[58:59] op_sel_hi:[1,0,1]
	v_xor_b32_e32 v58, 0x80000000, v91
	v_mov_b32_e32 v59, v91
	v_pk_mul_f32 v[58:59], v[56:57], v[58:59] op_sel:[1,0] op_sel_hi:[0,1]
	v_pk_fma_f32 v[58:59], v[56:57], v[90:91], v[58:59] op_sel_hi:[1,0,1]
	ds_write2_b64 v71, v[46:47], v[58:59] offset0:128 offset1:144
	v_xor_b32_e32 v46, 0x80000000, v57
	v_mov_b32_e32 v47, v57
	v_pk_mul_f32 v[46:47], v[16:17], v[46:47] op_sel:[1,0] op_sel_hi:[0,1]
	v_pk_fma_f32 v[46:47], v[16:17], v[56:57], v[46:47] op_sel_hi:[1,0,1]
	v_xor_b32_e32 v56, 0x80000000, v51
	v_mov_b32_e32 v57, v51
	v_pk_mul_f32 v[56:57], v[46:47], v[56:57] op_sel:[1,0] op_sel_hi:[0,1]
	v_pk_fma_f32 v[50:51], v[46:47], v[50:51], v[56:57] op_sel_hi:[1,0,1]
	v_xor_b32_e32 v56, 0x80000000, v47
	v_mov_b32_e32 v57, v47
	v_pk_mul_f32 v[56:57], v[16:17], v[56:57] op_sel:[1,0] op_sel_hi:[0,1]
	v_pk_fma_f32 v[46:47], v[16:17], v[46:47], v[56:57] op_sel_hi:[1,0,1]
	v_xor_b32_e32 v56, 0x80000000, v55
	v_mov_b32_e32 v57, v55
	v_pk_mul_f32 v[56:57], v[46:47], v[56:57] op_sel:[1,0] op_sel_hi:[0,1]
	v_pk_fma_f32 v[54:55], v[46:47], v[54:55], v[56:57] op_sel_hi:[1,0,1]
	ds_write2_b64 v70, v[50:51], v[54:55] offset0:160 offset1:176
	v_xor_b32_e32 v50, 0x80000000, v47
	v_mov_b32_e32 v51, v47
	v_pk_mul_f32 v[50:51], v[16:17], v[50:51] op_sel:[1,0] op_sel_hi:[0,1]
	v_pk_fma_f32 v[46:47], v[16:17], v[46:47], v[50:51] op_sel_hi:[1,0,1]
	v_xor_b32_e32 v50, 0x80000000, v39
	v_mov_b32_e32 v51, v39
	v_pk_mul_f32 v[50:51], v[50:51], v[46:47] op_sel:[0,1] op_sel_hi:[1,0]
	s_nop 0
	v_pk_fma_f32 v[38:39], v[38:39], v[46:47], v[50:51] op_sel_hi:[0,1,1]
	v_xor_b32_e32 v50, 0x80000000, v47
	v_mov_b32_e32 v51, v47
	v_pk_mul_f32 v[50:51], v[16:17], v[50:51] op_sel:[1,0] op_sel_hi:[0,1]
	v_pk_fma_f32 v[46:47], v[16:17], v[46:47], v[50:51] op_sel_hi:[1,0,1]
	v_xor_b32_e32 v50, 0x80000000, v77
	v_mov_b32_e32 v51, v77
	v_pk_mul_f32 v[50:51], v[46:47], v[50:51] op_sel:[1,0] op_sel_hi:[0,1]
	v_pk_fma_f32 v[50:51], v[46:47], v[76:77], v[50:51] op_sel_hi:[1,0,1]
	ds_write2_b64 v69, v[38:39], v[50:51] offset0:192 offset1:208
	v_xor_b32_e32 v38, 0x80000000, v47
	v_mov_b32_e32 v39, v47
	v_pk_mul_f32 v[38:39], v[16:17], v[38:39] op_sel:[1,0] op_sel_hi:[0,1]
	v_pk_fma_f32 v[38:39], v[16:17], v[46:47], v[38:39] op_sel_hi:[1,0,1]
	v_xor_b32_e32 v46, 0x80000000, v43
	v_mov_b32_e32 v47, v43
	v_pk_mul_f32 v[46:47], v[46:47], v[38:39] op_sel:[0,1] op_sel_hi:[1,0]
	s_nop 0
	v_pk_fma_f32 v[42:43], v[42:43], v[38:39], v[46:47] op_sel_hi:[0,1,1]
	v_xor_b32_e32 v46, 0x80000000, v39
	v_mov_b32_e32 v47, v39
	v_pk_mul_f32 v[46:47], v[16:17], v[46:47] op_sel:[1,0] op_sel_hi:[0,1]
	v_pk_fma_f32 v[38:39], v[16:17], v[38:39], v[46:47] op_sel_hi:[1,0,1]
	v_xor_b32_e32 v46, 0x80000000, v85
	v_mov_b32_e32 v47, v85
	v_pk_mul_f32 v[46:47], v[38:39], v[46:47] op_sel:[1,0] op_sel_hi:[0,1]
	v_pk_fma_f32 v[46:47], v[38:39], v[84:85], v[46:47] op_sel_hi:[1,0,1]
	ds_write2_b64 v68, v[42:43], v[46:47] offset0:224 offset1:240
	v_xor_b32_e32 v42, 0x80000000, v39
	v_mov_b32_e32 v43, v39
	v_pk_mul_f32 v[42:43], v[16:17], v[42:43] op_sel:[1,0] op_sel_hi:[0,1]
	v_pk_fma_f32 v[38:39], v[16:17], v[38:39], v[42:43] op_sel_hi:[1,0,1]
	v_xor_b32_e32 v42, 0x80000000, v31
	v_mov_b32_e32 v43, v31
	v_pk_mul_f32 v[42:43], v[42:43], v[38:39] op_sel:[0,1] op_sel_hi:[1,0]
	s_nop 0
	v_pk_fma_f32 v[30:31], v[30:31], v[38:39], v[42:43] op_sel_hi:[0,1,1]
	v_xor_b32_e32 v42, 0x80000000, v39
	v_mov_b32_e32 v43, v39
	v_pk_mul_f32 v[42:43], v[16:17], v[42:43] op_sel:[1,0] op_sel_hi:[0,1]
	v_pk_fma_f32 v[38:39], v[16:17], v[38:39], v[42:43] op_sel_hi:[1,0,1]
	v_xor_b32_e32 v42, 0x80000000, v79
	v_mov_b32_e32 v43, v79
	v_pk_mul_f32 v[42:43], v[42:43], v[38:39] op_sel:[0,1] op_sel_hi:[1,0]
	s_nop 0
	v_pk_fma_f32 v[42:43], v[78:79], v[38:39], v[42:43] op_sel_hi:[0,1,1]
	ds_write2_b64 v67, v[30:31], v[42:43] offset1:16
	v_xor_b32_e32 v30, 0x80000000, v39
	v_mov_b32_e32 v31, v39
	v_pk_mul_f32 v[30:31], v[16:17], v[30:31] op_sel:[1,0] op_sel_hi:[0,1]
	v_pk_fma_f32 v[30:31], v[16:17], v[38:39], v[30:31] op_sel_hi:[1,0,1]
	v_xor_b32_e32 v38, 0x80000000, v35
	v_mov_b32_e32 v39, v35
	v_pk_mul_f32 v[38:39], v[38:39], v[30:31] op_sel:[0,1] op_sel_hi:[1,0]
	s_nop 0
	v_pk_fma_f32 v[34:35], v[34:35], v[30:31], v[38:39] op_sel_hi:[0,1,1]
	v_xor_b32_e32 v38, 0x80000000, v31
	v_mov_b32_e32 v39, v31
	v_pk_mul_f32 v[38:39], v[16:17], v[38:39] op_sel:[1,0] op_sel_hi:[0,1]
	v_pk_fma_f32 v[30:31], v[16:17], v[30:31], v[38:39] op_sel_hi:[1,0,1]
	v_xor_b32_e32 v38, 0x80000000, v53
	v_mov_b32_e32 v39, v53
	v_pk_mul_f32 v[38:39], v[38:39], v[30:31] op_sel:[0,1] op_sel_hi:[1,0]
	s_nop 0
	v_pk_fma_f32 v[38:39], v[52:53], v[30:31], v[38:39] op_sel_hi:[0,1,1]
	ds_write2_b64 v66, v[34:35], v[38:39] offset0:32 offset1:48
	v_xor_b32_e32 v34, 0x80000000, v31
	v_mov_b32_e32 v35, v31
	v_pk_mul_f32 v[34:35], v[16:17], v[34:35] op_sel:[1,0] op_sel_hi:[0,1]
	v_pk_fma_f32 v[30:31], v[16:17], v[30:31], v[34:35] op_sel_hi:[1,0,1]
	v_xor_b32_e32 v34, 0x80000000, v27
	v_mov_b32_e32 v35, v27
	v_pk_mul_f32 v[34:35], v[34:35], v[30:31] op_sel:[0,1] op_sel_hi:[1,0]
	s_nop 0
	v_pk_fma_f32 v[26:27], v[26:27], v[30:31], v[34:35] op_sel_hi:[0,1,1]
	v_xor_b32_e32 v34, 0x80000000, v31
	v_mov_b32_e32 v35, v31
	v_pk_mul_f32 v[34:35], v[16:17], v[34:35] op_sel:[1,0] op_sel_hi:[0,1]
	v_pk_fma_f32 v[30:31], v[16:17], v[30:31], v[34:35] op_sel_hi:[1,0,1]
	v_xor_b32_e32 v34, 0x80000000, v49
	v_mov_b32_e32 v35, v49
	v_pk_mul_f32 v[34:35], v[34:35], v[30:31] op_sel:[0,1] op_sel_hi:[1,0]
	s_nop 0
	v_pk_fma_f32 v[34:35], v[48:49], v[30:31], v[34:35] op_sel_hi:[0,1,1]
	ds_write2_b64 v65, v[26:27], v[34:35] offset0:64 offset1:80
	v_xor_b32_e32 v26, 0x80000000, v31
	v_mov_b32_e32 v27, v31
	v_pk_mul_f32 v[26:27], v[16:17], v[26:27] op_sel:[1,0] op_sel_hi:[0,1]
	v_pk_fma_f32 v[26:27], v[16:17], v[30:31], v[26:27] op_sel_hi:[1,0,1]
	v_xor_b32_e32 v30, 0x80000000, v29
	v_mov_b32_e32 v31, v29
	v_pk_mul_f32 v[30:31], v[30:31], v[26:27] op_sel:[0,1] op_sel_hi:[1,0]
	s_nop 0
	v_pk_fma_f32 v[28:29], v[28:29], v[26:27], v[30:31] op_sel_hi:[0,1,1]
	v_xor_b32_e32 v30, 0x80000000, v27
	v_mov_b32_e32 v31, v27
	v_pk_mul_f32 v[30:31], v[16:17], v[30:31] op_sel:[1,0] op_sel_hi:[0,1]
	v_pk_fma_f32 v[26:27], v[16:17], v[26:27], v[30:31] op_sel_hi:[1,0,1]
	v_xor_b32_e32 v30, 0x80000000, v81
	v_mov_b32_e32 v31, v81
	v_pk_mul_f32 v[30:31], v[30:31], v[26:27] op_sel:[0,1] op_sel_hi:[1,0]
	s_nop 0
	v_pk_fma_f32 v[30:31], v[80:81], v[26:27], v[30:31] op_sel_hi:[0,1,1]
	ds_write2_b64 v64, v[28:29], v[30:31] offset0:96 offset1:112
	v_xor_b32_e32 v28, 0x80000000, v27
	v_mov_b32_e32 v29, v27
	v_pk_mul_f32 v[28:29], v[16:17], v[28:29] op_sel:[1,0] op_sel_hi:[0,1]
	v_pk_fma_f32 v[26:27], v[16:17], v[26:27], v[28:29] op_sel_hi:[1,0,1]
	v_xor_b32_e32 v28, 0x80000000, v23
	v_mov_b32_e32 v29, v23
	v_pk_mul_f32 v[28:29], v[28:29], v[26:27] op_sel:[0,1] op_sel_hi:[1,0]
	s_nop 0
	v_pk_fma_f32 v[22:23], v[22:23], v[26:27], v[28:29] op_sel_hi:[0,1,1]
	v_xor_b32_e32 v28, 0x80000000, v27
	v_mov_b32_e32 v29, v27
	v_pk_mul_f32 v[28:29], v[16:17], v[28:29] op_sel:[1,0] op_sel_hi:[0,1]
	v_pk_fma_f32 v[26:27], v[16:17], v[26:27], v[28:29] op_sel_hi:[1,0,1]
	v_xor_b32_e32 v28, 0x80000000, v41
	v_mov_b32_e32 v29, v41
	v_pk_mul_f32 v[28:29], v[28:29], v[26:27] op_sel:[0,1] op_sel_hi:[1,0]
	s_nop 0
	v_pk_fma_f32 v[28:29], v[40:41], v[26:27], v[28:29] op_sel_hi:[0,1,1]
	ds_write2_b64 v63, v[22:23], v[28:29] offset0:128 offset1:144
	v_xor_b32_e32 v22, 0x80000000, v27
	v_mov_b32_e32 v23, v27
	v_pk_mul_f32 v[22:23], v[16:17], v[22:23] op_sel:[1,0] op_sel_hi:[0,1]
	v_pk_fma_f32 v[22:23], v[16:17], v[26:27], v[22:23] op_sel_hi:[1,0,1]
	v_xor_b32_e32 v26, 0x80000000, v25
	v_mov_b32_e32 v27, v25
	v_pk_mul_f32 v[26:27], v[26:27], v[22:23] op_sel:[0,1] op_sel_hi:[1,0]
	s_nop 0
	v_pk_fma_f32 v[24:25], v[24:25], v[22:23], v[26:27] op_sel_hi:[0,1,1]
	v_xor_b32_e32 v26, 0x80000000, v23
	v_mov_b32_e32 v27, v23
	v_pk_mul_f32 v[26:27], v[16:17], v[26:27] op_sel:[1,0] op_sel_hi:[0,1]
	v_pk_fma_f32 v[22:23], v[16:17], v[22:23], v[26:27] op_sel_hi:[1,0,1]
	v_xor_b32_e32 v26, 0x80000000, v45
	v_mov_b32_e32 v27, v45
	v_pk_mul_f32 v[26:27], v[26:27], v[22:23] op_sel:[0,1] op_sel_hi:[1,0]
	s_nop 0
	v_pk_fma_f32 v[26:27], v[44:45], v[22:23], v[26:27] op_sel_hi:[0,1,1]
	ds_write2_b64 v62, v[24:25], v[26:27] offset0:160 offset1:176
	v_xor_b32_e32 v24, 0x80000000, v23
	v_mov_b32_e32 v25, v23
	v_pk_mul_f32 v[24:25], v[16:17], v[24:25] op_sel:[1,0] op_sel_hi:[0,1]
	v_pk_fma_f32 v[22:23], v[16:17], v[22:23], v[24:25] op_sel_hi:[1,0,1]
	v_xor_b32_e32 v24, 0x80000000, v19
	v_mov_b32_e32 v25, v19
	v_pk_mul_f32 v[24:25], v[24:25], v[22:23] op_sel:[0,1] op_sel_hi:[1,0]
	s_nop 0
	v_pk_fma_f32 v[18:19], v[18:19], v[22:23], v[24:25] op_sel_hi:[0,1,1]
	v_xor_b32_e32 v24, 0x80000000, v23
	v_mov_b32_e32 v25, v23
	v_pk_mul_f32 v[24:25], v[16:17], v[24:25] op_sel:[1,0] op_sel_hi:[0,1]
	v_pk_fma_f32 v[22:23], v[16:17], v[22:23], v[24:25] op_sel_hi:[1,0,1]
	v_xor_b32_e32 v24, 0x80000000, v33
	v_mov_b32_e32 v25, v33
	v_pk_mul_f32 v[24:25], v[24:25], v[22:23] op_sel:[0,1] op_sel_hi:[1,0]
	s_nop 0
	v_pk_fma_f32 v[24:25], v[32:33], v[22:23], v[24:25] op_sel_hi:[0,1,1]
	ds_write2_b64 v15, v[18:19], v[24:25] offset0:192 offset1:208
	v_xor_b32_e32 v18, 0x80000000, v23
	v_mov_b32_e32 v19, v23
	v_pk_mul_f32 v[18:19], v[16:17], v[18:19] op_sel:[1,0] op_sel_hi:[0,1]
	v_pk_fma_f32 v[18:19], v[16:17], v[22:23], v[18:19] op_sel_hi:[1,0,1]
	v_xor_b32_e32 v22, 0x80000000, v21
	v_mov_b32_e32 v23, v21
	v_pk_mul_f32 v[22:23], v[22:23], v[18:19] op_sel:[0,1] op_sel_hi:[1,0]
	s_nop 0
	v_pk_fma_f32 v[20:21], v[20:21], v[18:19], v[22:23] op_sel_hi:[0,1,1]
	v_xor_b32_e32 v22, 0x80000000, v19
	v_mov_b32_e32 v23, v19
	v_pk_mul_f32 v[22:23], v[16:17], v[22:23] op_sel:[1,0] op_sel_hi:[0,1]
	v_pk_fma_f32 v[16:17], v[16:17], v[18:19], v[22:23] op_sel_hi:[1,0,1]
	v_xor_b32_e32 v18, 0x80000000, v37
	v_mov_b32_e32 v19, v37
	v_pk_mul_f32 v[18:19], v[18:19], v[16:17] op_sel:[0,1] op_sel_hi:[1,0]
	s_nop 0
	v_pk_fma_f32 v[16:17], v[36:37], v[16:17], v[18:19] op_sel_hi:[0,1,1]
	ds_write2_b64 v13, v[20:21], v[16:17] offset0:224 offset1:240
	v_mov_b32_e32 v16, v182
	v_mov_b32_e32 v10, v176
	v_mov_b32_e32 v17, v175
	s_waitcnt lgkmcnt(0)
	s_barrier
	v_lshlrev_b32_e32 v190, 3, v16
	v_add_u32_e32 v190, 0x1000, v190
	global_load_dwordx2 v[202:203], v190, s[46:47] offset:-4096
	global_load_dwordx2 v[204:205], v190, s[46:47]
	v_add_u32_e32 v190, 0x2000, v190
	global_load_dwordx2 v[206:207], v190, s[46:47] offset:-4096
	global_load_dwordx2 v[208:209], v190, s[46:47]
	v_add_u32_e32 v190, 0x2000, v190
	global_load_dwordx2 v[210:211], v190, s[46:47] offset:-4096
	global_load_dwordx2 v[212:213], v190, s[46:47]
	v_add_u32_e32 v190, 0x2000, v190
	global_load_dwordx2 v[214:215], v190, s[46:47] offset:-4096
	global_load_dwordx2 v[216:217], v190, s[46:47]
	v_add_u32_e32 v190, 0x2000, v190
	global_load_dwordx2 v[218:219], v190, s[46:47] offset:-4096
	global_load_dwordx2 v[220:221], v190, s[46:47]
	v_add_u32_e32 v190, 0x2000, v190
	global_load_dwordx2 v[222:223], v190, s[46:47] offset:-4096
	global_load_dwordx2 v[224:225], v190, s[46:47]
	v_add_u32_e32 v190, 0x2000, v190
	global_load_dwordx2 v[226:227], v190, s[46:47] offset:-4096
	global_load_dwordx2 v[228:229], v190, s[46:47]
	v_add_u32_e32 v190, 0x2000, v190
	global_load_dwordx2 v[230:231], v190, s[46:47] offset:-4096
	global_load_dwordx2 v[232:233], v190, s[46:47]
	v_mov_b32_e32 v50, v165
	v_lshlrev_b32_e32 v13, 3, v17
	v_lshlrev_b32_e32 v48, 3, v10
	v_add3_u32 v10, 0, v13, v48
	v_xor_b32_e32 v13, 1, v17
	v_xor_b32_e32 v34, 8, v17
	v_xor_b32_e32 v36, 9, v17
	v_lshlrev_b32_e32 v13, 3, v13
	v_xor_b32_e32 v15, 2, v17
	v_xor_b32_e32 v24, 3, v17
	v_xor_b32_e32 v26, 4, v17
	v_xor_b32_e32 v28, 5, v17
	v_xor_b32_e32 v30, 6, v17
	v_xor_b32_e32 v32, 7, v17
	v_lshlrev_b32_e32 v34, 3, v34
	v_lshlrev_b32_e32 v36, 3, v36
	v_xor_b32_e32 v38, 10, v17
	v_xor_b32_e32 v40, 11, v17
	v_xor_b32_e32 v42, 12, v17
	v_xor_b32_e32 v44, 13, v17
	v_xor_b32_e32 v46, 14, v17
	v_xor_b32_e32 v17, 15, v17
	v_add3_u32 v13, 0, v13, v48
	v_lshlrev_b32_e32 v15, 3, v15
	v_lshlrev_b32_e32 v24, 3, v24
	v_lshlrev_b32_e32 v26, 3, v26
	v_lshlrev_b32_e32 v28, 3, v28
	v_lshlrev_b32_e32 v30, 3, v30
	v_lshlrev_b32_e32 v32, 3, v32
	v_add3_u32 v57, 0, v34, v48
	v_add3_u32 v58, 0, v36, v48
	v_lshlrev_b32_e32 v38, 3, v38
	v_lshlrev_b32_e32 v40, 3, v40
	v_lshlrev_b32_e32 v42, 3, v42
	v_lshlrev_b32_e32 v44, 3, v44
	v_lshlrev_b32_e32 v46, 3, v46
	v_lshlrev_b32_e32 v17, 3, v17
	ds_read_b64 v[18:19], v10
	ds_read_b64 v[20:21], v13
	v_add3_u32 v15, 0, v15, v48
	v_add3_u32 v52, 0, v24, v48
	v_add3_u32 v53, 0, v26, v48
	v_add3_u32 v54, 0, v28, v48
	v_add3_u32 v55, 0, v30, v48
	v_add3_u32 v56, 0, v32, v48
	ds_read_b64 v[34:35], v57
	ds_read_b64 v[36:37], v58
	v_add3_u32 v59, 0, v38, v48
	v_add3_u32 v60, 0, v40, v48
	v_add3_u32 v61, 0, v42, v48
	v_add3_u32 v62, 0, v44, v48
	v_add3_u32 v63, 0, v46, v48
	v_add3_u32 v64, 0, v17, v48
	v_mov_b32_e32 v17, v1
	ds_read_b64 v[22:23], v15
	ds_read_b64 v[24:25], v52
	ds_read_b64 v[26:27], v53
	ds_read_b64 v[28:29], v54
	ds_read_b64 v[30:31], v55
	ds_read_b64 v[32:33], v56
	ds_read_b64 v[38:39], v59
	ds_read_b64 v[40:41], v60
	ds_read_b64 v[42:43], v61
	ds_read_b64 v[44:45], v62
	ds_read_b64 v[46:47], v63
	ds_read_b64 v[48:49], v64
	s_waitcnt lgkmcnt(13)
	v_pk_add_f32 v[70:71], v[18:19], v[34:35]
	v_mov_b32_e32 v17, v164
	v_pk_add_f32 v[18:19], v[18:19], v[34:35] neg_lo:[0,1] neg_hi:[0,1]
	v_mov_b32_e32 v17, v166
	s_waitcnt lgkmcnt(12)
	v_pk_add_f32 v[34:35], v[20:21], v[36:37]
	v_pk_add_f32 v[20:21], v[20:21], v[36:37] neg_lo:[0,1] neg_hi:[0,1]
	v_mov_b32_e32 v66, v167
	v_mov_b32_e32 v17, v168
	v_mov_b32_e32 v68, v169
	v_xor_b32_e32 v36, 0x80000000, v21
	v_mov_b32_e32 v37, v20
	s_nop 0
	v_pk_mul_f32 v[36:37], v[36:37], v[68:69] op_sel_hi:[1,0] neg_lo:[0,1] neg_hi:[0,1]
	v_mov_b32_e32 v17, v170
	v_pk_fma_f32 v[20:21], v[20:21], v[50:51], v[36:37] op_sel_hi:[1,0,1]
	s_waitcnt lgkmcnt(5)
	v_pk_add_f32 v[36:37], v[22:23], v[38:39]
	v_pk_add_f32 v[22:23], v[22:23], v[38:39] neg_lo:[0,1] neg_hi:[0,1]
	s_nop 0
	v_xor_b32_e32 v38, 0x80000000, v23
	v_mov_b32_e32 v39, v22
	v_pk_mul_f32 v[38:39], v[38:39], v[66:67] op_sel_hi:[1,0] neg_lo:[0,1] neg_hi:[0,1]
	v_mov_b32_e32 v17, v171
	v_pk_fma_f32 v[22:23], v[22:23], v[66:67], v[38:39] op_sel_hi:[1,0,1]
	s_waitcnt lgkmcnt(4)
	v_pk_add_f32 v[38:39], v[24:25], v[40:41]
	v_pk_add_f32 v[24:25], v[24:25], v[40:41] neg_lo:[0,1] neg_hi:[0,1]
	s_nop 0
	v_pk_mul_f32 v[40:41], v[24:25], v[68:69] op_sel_hi:[1,0]
	v_xor_b32_e32 v72, 0x80000000, v25
	v_mov_b32_e32 v73, v24
	v_pk_fma_f32 v[24:25], v[72:73], v[50:51], v[40:41] op_sel_hi:[1,0,1] neg_lo:[0,1,0] neg_hi:[0,1,0]
	s_waitcnt lgkmcnt(3)
	v_pk_add_f32 v[40:41], v[26:27], v[42:43]
	v_pk_add_f32 v[26:27], v[26:27], v[42:43] neg_lo:[0,1] neg_hi:[0,1]
	v_ashrrev_i32_e32 v17, 31, v16
	v_xor_b32_e32 v73, 0x80000000, v26
	v_mov_b32_e32 v72, v27
	s_waitcnt lgkmcnt(2)
	v_pk_add_f32 v[26:27], v[28:29], v[44:45]
	v_pk_add_f32 v[28:29], v[28:29], v[44:45] neg_lo:[0,1] neg_hi:[0,1]
	s_nop 0
	v_pk_mul_f32 v[42:43], v[28:29], v[68:69] op_sel_hi:[1,0] neg_lo:[0,1] neg_hi:[0,1]
	v_xor_b32_e32 v44, 0x80000000, v29
	v_mov_b32_e32 v45, v28
	v_pk_fma_f32 v[28:29], v[44:45], v[50:51], v[42:43] op_sel_hi:[1,0,1] neg_lo:[0,1,0] neg_hi:[0,1,0]
	s_waitcnt lgkmcnt(1)
	v_pk_add_f32 v[42:43], v[30:31], v[46:47]
	v_pk_add_f32 v[30:31], v[30:31], v[46:47] neg_lo:[0,1] neg_hi:[0,1]
	s_nop 0
	v_xor_b32_e32 v44, 0x80000000, v31
	v_mov_b32_e32 v45, v30
	v_pk_mul_f32 v[44:45], v[44:45], v[66:67] op_sel_hi:[1,0] neg_lo:[0,1] neg_hi:[0,1]
	s_nop 0
	v_pk_fma_f32 v[30:31], v[30:31], v[66:67], v[44:45] op_sel_hi:[1,0,1] neg_lo:[0,1,0] neg_hi:[0,1,0]
	s_waitcnt lgkmcnt(0)
	v_pk_add_f32 v[44:45], v[32:33], v[48:49]
	v_pk_add_f32 v[32:33], v[32:33], v[48:49] neg_lo:[0,1] neg_hi:[0,1]
	v_pk_add_f32 v[48:49], v[34:35], v[26:27]
	v_pk_add_f32 v[26:27], v[34:35], v[26:27] neg_lo:[0,1] neg_hi:[0,1]
	v_xor_b32_e32 v46, 0x80000000, v33
	v_xor_b32_e32 v34, 0x80000000, v27
	v_mov_b32_e32 v35, v26
	v_pk_mul_f32 v[34:35], v[34:35], v[66:67] op_sel_hi:[1,0] neg_lo:[0,1] neg_hi:[0,1]
	v_mov_b32_e32 v47, v32
	v_pk_fma_f32 v[26:27], v[26:27], v[66:67], v[34:35] op_sel_hi:[1,0,1]
	v_pk_add_f32 v[34:35], v[36:37], v[42:43]
	v_pk_add_f32 v[36:37], v[36:37], v[42:43] neg_lo:[0,1] neg_hi:[0,1]
	v_pk_mul_f32 v[46:47], v[46:47], v[68:69] op_sel_hi:[1,0] neg_lo:[0,1] neg_hi:[0,1]
	v_xor_b32_e32 v43, 0x80000000, v36
	v_mov_b32_e32 v42, v37
	v_pk_add_f32 v[36:37], v[38:39], v[44:45]
	v_pk_add_f32 v[38:39], v[38:39], v[44:45] neg_lo:[0,1] neg_hi:[0,1]
	v_pk_fma_f32 v[46:47], v[32:33], v[50:51], v[46:47] op_sel_hi:[1,0,1] neg_lo:[0,1,0] neg_hi:[0,1,0]
	v_xor_b32_e32 v44, 0x80000000, v39
	v_mov_b32_e32 v45, v38
	v_pk_add_f32 v[32:33], v[70:71], v[40:41]
	v_pk_mul_f32 v[44:45], v[44:45], v[66:67] op_sel_hi:[1,0] neg_lo:[0,1] neg_hi:[0,1]
	v_pk_add_f32 v[40:41], v[70:71], v[40:41] neg_lo:[0,1] neg_hi:[0,1]
	v_pk_fma_f32 v[38:39], v[38:39], v[66:67], v[44:45] op_sel_hi:[1,0,1] neg_lo:[0,1,0] neg_hi:[0,1,0]
	v_pk_add_f32 v[44:45], v[32:33], v[34:35]
	v_pk_add_f32 v[32:33], v[32:33], v[34:35] neg_lo:[0,1] neg_hi:[0,1]
	v_pk_add_f32 v[34:35], v[48:49], v[36:37]
	v_pk_add_f32 v[36:37], v[48:49], v[36:37] neg_lo:[0,1] neg_hi:[0,1]
	v_pk_add_f32 v[50:51], v[44:45], v[34:35]
	v_xor_b32_e32 v49, 0x80000000, v36
	v_mov_b32_e32 v48, v37
	v_pk_add_f32 v[36:37], v[44:45], v[34:35] neg_lo:[0,1] neg_hi:[0,1]
	v_pk_add_f32 v[68:69], v[32:33], v[48:49]
	v_pk_add_f32 v[44:45], v[32:33], v[48:49] neg_lo:[0,1] neg_hi:[0,1]
	v_pk_add_f32 v[32:33], v[40:41], v[42:43]
	v_pk_add_f32 v[34:35], v[40:41], v[42:43] neg_lo:[0,1] neg_hi:[0,1]
	v_pk_add_f32 v[40:41], v[26:27], v[38:39]
	v_pk_add_f32 v[26:27], v[26:27], v[38:39] neg_lo:[0,1] neg_hi:[0,1]
	v_pk_add_f32 v[42:43], v[32:33], v[40:41] neg_lo:[0,1] neg_hi:[0,1]
	v_xor_b32_e32 v39, 0x80000000, v26
	v_mov_b32_e32 v38, v27
	v_pk_add_f32 v[26:27], v[32:33], v[40:41]
	v_pk_add_f32 v[40:41], v[20:21], v[28:29]
	v_pk_add_f32 v[20:21], v[20:21], v[28:29] neg_lo:[0,1] neg_hi:[0,1]
	v_pk_add_f32 v[32:33], v[34:35], v[38:39]
	v_xor_b32_e32 v28, 0x80000000, v21
	v_mov_b32_e32 v29, v20
	v_pk_mul_f32 v[28:29], v[66:67], v[28:29] op_sel_hi:[0,1] neg_lo:[1,0] neg_hi:[1,0]
	v_pk_fma_f32 v[20:21], v[66:67], v[20:21], v[28:29] op_sel_hi:[0,1,1]
	v_pk_add_f32 v[28:29], v[22:23], v[30:31]
	v_pk_add_f32 v[22:23], v[22:23], v[30:31] neg_lo:[0,1] neg_hi:[0,1]
	v_pk_add_f32 v[38:39], v[34:35], v[38:39] neg_lo:[0,1] neg_hi:[0,1]
	v_xor_b32_e32 v31, 0x80000000, v22
	v_mov_b32_e32 v30, v23
	v_pk_add_f32 v[22:23], v[24:25], v[46:47]
	v_pk_add_f32 v[24:25], v[24:25], v[46:47] neg_lo:[0,1] neg_hi:[0,1]
	v_pk_add_f32 v[34:35], v[18:19], v[72:73]
	v_xor_b32_e32 v46, 0x80000000, v25
	v_mov_b32_e32 v47, v24
	v_pk_mul_f32 v[46:47], v[66:67], v[46:47] op_sel_hi:[0,1] neg_lo:[1,0] neg_hi:[1,0]
	v_pk_fma_f32 v[24:25], v[66:67], v[24:25], v[46:47] op_sel_hi:[0,1,1] neg_lo:[1,0,0] neg_hi:[1,0,0]
	v_pk_add_f32 v[46:47], v[34:35], v[28:29]
	v_pk_add_f32 v[28:29], v[34:35], v[28:29] neg_lo:[0,1] neg_hi:[0,1]
	v_pk_add_f32 v[34:35], v[40:41], v[22:23]
	v_pk_add_f32 v[22:23], v[40:41], v[22:23] neg_lo:[0,1] neg_hi:[0,1]
	v_pk_add_f32 v[18:19], v[18:19], v[72:73] neg_lo:[0,1] neg_hi:[0,1]
	v_xor_b32_e32 v49, 0x80000000, v22
	v_mov_b32_e32 v48, v23
	v_pk_add_f32 v[66:67], v[28:29], v[48:49]
	v_pk_add_f32 v[48:49], v[28:29], v[48:49] neg_lo:[0,1] neg_hi:[0,1]
	v_pk_add_f32 v[28:29], v[18:19], v[30:31]
	v_pk_add_f32 v[18:19], v[18:19], v[30:31] neg_lo:[0,1] neg_hi:[0,1]
	v_pk_add_f32 v[30:31], v[20:21], v[24:25]
	v_pk_add_f32 v[20:21], v[20:21], v[24:25] neg_lo:[0,1] neg_hi:[0,1]
	v_pk_add_f32 v[22:23], v[46:47], v[34:35]
	v_xor_b32_e32 v25, 0x80000000, v20
	v_mov_b32_e32 v24, v21
	v_lshl_add_u64 v[20:21], v[16:17], 3, s[46:47]
	s_waitcnt vmcnt(0)
	v_mov_b32_e32 v20, v202
	v_mov_b32_e32 v21, v203
	v_pk_add_f32 v[40:41], v[46:47], v[34:35] neg_lo:[0,1] neg_hi:[0,1]
	v_pk_add_f32 v[34:35], v[18:19], v[24:25]
	v_pk_add_f32 v[18:19], v[18:19], v[24:25] neg_lo:[0,1] neg_hi:[0,1]
	v_xor_b32_e32 v24, 0x80000000, v51
	v_mov_b32_e32 v25, v51
	v_pk_add_f32 v[70:71], v[28:29], v[30:31]
	v_pk_add_f32 v[46:47], v[28:29], v[30:31] neg_lo:[0,1] neg_hi:[0,1]
	v_xor_b32_e32 v28, 0x80000000, v23
	v_mov_b32_e32 v29, v23
	v_xor_b32_e32 v30, 0x80000000, v69
	v_mov_b32_e32 v31, v69
	v_mov_b32_e32 v17, v1
	s_nop 0
	v_pk_mul_f32 v[24:25], v[24:25], v[20:21] op_sel:[0,1] op_sel_hi:[1,0]
	s_nop 0
	v_pk_fma_f32 v[20:21], v[50:51], v[20:21], v[24:25] op_sel_hi:[0,1,1]
	v_add_u32_e32 v24, 0x200, v16
	v_ashrrev_i32_e32 v25, 31, v24
	v_lshl_add_u64 v[24:25], v[24:25], 3, s[46:47]
	v_mov_b32_e32 v24, v204
	v_mov_b32_e32 v25, v205
	v_xor_b32_e32 v50, 0x80000000, v67
	v_mov_b32_e32 v51, v67
	s_nop 0
	v_pk_mul_f32 v[28:29], v[24:25], v[28:29] op_sel:[1,0] op_sel_hi:[0,1]
	v_pk_fma_f32 v[22:23], v[24:25], v[22:23], v[28:29] op_sel_hi:[1,0,1]
	v_add_u32_e32 v24, 0x400, v16
	v_ashrrev_i32_e32 v25, 31, v24
	v_lshl_add_u64 v[24:25], v[24:25], 3, s[46:47]
	v_mov_b32_e32 v24, v206
	v_mov_b32_e32 v25, v207
	v_xor_b32_e32 v28, 0x80000000, v27
	v_mov_b32_e32 v29, v27
	s_nop 0
	v_pk_mul_f32 v[28:29], v[28:29], v[24:25] op_sel:[0,1] op_sel_hi:[1,0]
	s_nop 0
	v_pk_fma_f32 v[24:25], v[26:27], v[24:25], v[28:29] op_sel_hi:[0,1,1]
	v_add_u32_e32 v26, 0x600, v16
	v_ashrrev_i32_e32 v27, 31, v26
	v_lshl_add_u64 v[26:27], v[26:27], 3, s[46:47]
	v_mov_b32_e32 v26, v208
	v_mov_b32_e32 v27, v209
	v_xor_b32_e32 v28, 0x80000000, v71
	v_mov_b32_e32 v29, v71
	s_nop 0
	v_pk_mul_f32 v[28:29], v[26:27], v[28:29] op_sel:[1,0] op_sel_hi:[0,1]
	v_pk_fma_f32 v[26:27], v[26:27], v[70:71], v[28:29] op_sel_hi:[1,0,1]
	v_add_u32_e32 v28, 0x800, v16
	v_ashrrev_i32_e32 v29, 31, v28
	v_lshl_add_u64 v[28:29], v[28:29], 3, s[46:47]
	v_mov_b32_e32 v28, v210
	v_mov_b32_e32 v29, v211
	s_nop 0
	v_pk_mul_f32 v[30:31], v[30:31], v[28:29] op_sel:[0,1] op_sel_hi:[1,0]
	s_nop 0
	v_pk_fma_f32 v[28:29], v[68:69], v[28:29], v[30:31] op_sel_hi:[0,1,1]
	v_add_u32_e32 v30, 0xa00, v16
	v_ashrrev_i32_e32 v31, 31, v30
	v_lshl_add_u64 v[30:31], v[30:31], 3, s[46:47]
	v_mov_b32_e32 v30, v212
	v_mov_b32_e32 v31, v213
	v_mov_b32_e32 v68, v169
	s_nop 0
	v_pk_mul_f32 v[50:51], v[30:31], v[50:51] op_sel:[1,0] op_sel_hi:[0,1]
	v_pk_fma_f32 v[30:31], v[30:31], v[66:67], v[50:51] op_sel_hi:[1,0,1]
	v_add_u32_e32 v50, 0xc00, v16
	v_ashrrev_i32_e32 v51, 31, v50
	v_lshl_add_u64 v[50:51], v[50:51], 3, s[46:47]
	v_mov_b32_e32 v50, v214
	v_mov_b32_e32 v51, v215
	v_xor_b32_e32 v66, 0x80000000, v33
	v_mov_b32_e32 v67, v33
	s_nop 0
	v_pk_mul_f32 v[66:67], v[66:67], v[50:51] op_sel:[0,1] op_sel_hi:[1,0]
	s_nop 0
	v_pk_fma_f32 v[32:33], v[32:33], v[50:51], v[66:67] op_sel_hi:[0,1,1]
	v_add_u32_e32 v50, 0xe00, v16
	v_ashrrev_i32_e32 v51, 31, v50
	v_lshl_add_u64 v[50:51], v[50:51], 3, s[46:47]
	v_mov_b32_e32 v50, v216
	v_mov_b32_e32 v51, v217
	v_xor_b32_e32 v66, 0x80000000, v35
	v_mov_b32_e32 v67, v35
	s_nop 0
	v_pk_mul_f32 v[66:67], v[50:51], v[66:67] op_sel:[1,0] op_sel_hi:[0,1]
	v_pk_fma_f32 v[34:35], v[50:51], v[34:35], v[66:67] op_sel_hi:[1,0,1]
	v_add_u32_e32 v50, 0x1000, v16
	v_ashrrev_i32_e32 v51, 31, v50
	v_lshl_add_u64 v[50:51], v[50:51], 3, s[46:47]
	v_mov_b32_e32 v50, v218
	v_mov_b32_e32 v51, v219
	v_xor_b32_e32 v66, 0x80000000, v37
	v_mov_b32_e32 v67, v37
	s_nop 0
	v_pk_mul_f32 v[66:67], v[66:67], v[50:51] op_sel:[0,1] op_sel_hi:[1,0]
	s_nop 0
	v_pk_fma_f32 v[36:37], v[36:37], v[50:51], v[66:67] op_sel_hi:[0,1,1]
	v_add_u32_e32 v50, 0x1200, v16
	v_ashrrev_i32_e32 v51, 31, v50
	v_lshl_add_u64 v[50:51], v[50:51], 3, s[46:47]
	v_mov_b32_e32 v50, v220
	v_mov_b32_e32 v51, v221
	v_xor_b32_e32 v66, 0x80000000, v41
	v_mov_b32_e32 v67, v41
	v_pk_add_f32 v[70:71], v[20:21], v[36:37]
	v_pk_add_f32 v[20:21], v[20:21], v[36:37] neg_lo:[0,1] neg_hi:[0,1]
	s_nop 0
	v_pk_mul_f32 v[66:67], v[66:67], v[50:51] op_sel:[0,1] op_sel_hi:[1,0]
	s_nop 0
	v_pk_fma_f32 v[40:41], v[40:41], v[50:51], v[66:67] op_sel_hi:[0,1,1]
	v_add_u32_e32 v50, 0x1400, v16
	v_ashrrev_i32_e32 v51, 31, v50
	v_lshl_add_u64 v[50:51], v[50:51], 3, s[46:47]
	v_mov_b32_e32 v50, v222
	v_mov_b32_e32 v51, v223
	v_xor_b32_e32 v66, 0x80000000, v43
	v_mov_b32_e32 v67, v43
	v_pk_add_f32 v[36:37], v[22:23], v[40:41]
	v_pk_add_f32 v[22:23], v[22:23], v[40:41] neg_lo:[0,1] neg_hi:[0,1]
	s_nop 0
	v_pk_mul_f32 v[66:67], v[66:67], v[50:51] op_sel:[0,1] op_sel_hi:[1,0]
	s_nop 0
	v_pk_fma_f32 v[42:43], v[42:43], v[50:51], v[66:67] op_sel_hi:[0,1,1]
	v_add_u32_e32 v50, 0x1600, v16
	v_ashrrev_i32_e32 v51, 31, v50
	v_lshl_add_u64 v[50:51], v[50:51], 3, s[46:47]
	v_mov_b32_e32 v50, v224
	v_mov_b32_e32 v51, v225
	v_xor_b32_e32 v66, 0x80000000, v47
	v_mov_b32_e32 v67, v47
	v_xor_b32_e32 v40, 0x80000000, v23
	v_mov_b32_e32 v41, v22
	s_nop 0
	v_pk_mul_f32 v[66:67], v[66:67], v[50:51] op_sel:[0,1] op_sel_hi:[1,0]
	s_nop 0
	v_pk_fma_f32 v[46:47], v[46:47], v[50:51], v[66:67] op_sel_hi:[0,1,1]
	v_add_u32_e32 v50, 0x1800, v16
	v_ashrrev_i32_e32 v51, 31, v50
	v_lshl_add_u64 v[50:51], v[50:51], 3, s[46:47]
	v_mov_b32_e32 v50, v226
	v_mov_b32_e32 v51, v227
	v_xor_b32_e32 v66, 0x80000000, v45
	v_mov_b32_e32 v67, v45
	s_nop 0
	v_pk_mul_f32 v[66:67], v[66:67], v[50:51] op_sel:[0,1] op_sel_hi:[1,0]
	s_nop 0
	v_pk_fma_f32 v[44:45], v[44:45], v[50:51], v[66:67] op_sel_hi:[0,1,1]
	v_add_u32_e32 v50, 0x1a00, v16
	v_ashrrev_i32_e32 v51, 31, v50
	v_lshl_add_u64 v[50:51], v[50:51], 3, s[46:47]
	v_mov_b32_e32 v50, v228
	v_mov_b32_e32 v51, v229
	v_xor_b32_e32 v66, 0x80000000, v49
	v_mov_b32_e32 v67, v49
	s_nop 0
	v_pk_mul_f32 v[66:67], v[66:67], v[50:51] op_sel:[0,1] op_sel_hi:[1,0]
	s_nop 0
	v_pk_fma_f32 v[48:49], v[48:49], v[50:51], v[66:67] op_sel_hi:[0,1,1]
	v_add_u32_e32 v50, 0x1c00, v16
	v_ashrrev_i32_e32 v51, 31, v50
	v_lshl_add_u64 v[50:51], v[50:51], 3, s[46:47]
	v_mov_b32_e32 v50, v230
	v_mov_b32_e32 v51, v231
	v_xor_b32_e32 v66, 0x80000000, v39
	v_mov_b32_e32 v67, v39
	s_nop 0
	v_pk_mul_f32 v[66:67], v[66:67], v[50:51] op_sel:[0,1] op_sel_hi:[1,0]
	s_nop 0
	v_pk_fma_f32 v[38:39], v[38:39], v[50:51], v[66:67] op_sel_hi:[0,1,1]
	v_add_u32_e32 v50, 0x1e00, v16
	v_ashrrev_i32_e32 v51, 31, v50
	v_lshl_add_u64 v[50:51], v[50:51], 3, s[46:47]
	v_mov_b32_e32 v50, v232
	v_mov_b32_e32 v51, v233
	v_lshlrev_b32_e32 v190, 3, v16
	v_add_u32_e32 v190, 0x11000, v190
	global_load_dwordx2 v[202:203], v190, s[46:47] offset:-4096
	global_load_dwordx2 v[204:205], v190, s[46:47]
	v_add_u32_e32 v190, 0x2000, v190
	global_load_dwordx2 v[206:207], v190, s[46:47] offset:-4096
	global_load_dwordx2 v[208:209], v190, s[46:47]
	v_add_u32_e32 v190, 0x2000, v190
	global_load_dwordx2 v[210:211], v190, s[46:47] offset:-4096
	global_load_dwordx2 v[212:213], v190, s[46:47]
	v_add_u32_e32 v190, 0x2000, v190
	global_load_dwordx2 v[214:215], v190, s[46:47] offset:-4096
	global_load_dwordx2 v[216:217], v190, s[46:47]
	v_add_u32_e32 v190, 0x2000, v190
	global_load_dwordx2 v[218:219], v190, s[46:47] offset:-4096
	global_load_dwordx2 v[220:221], v190, s[46:47]
	v_add_u32_e32 v190, 0x2000, v190
	global_load_dwordx2 v[222:223], v190, s[46:47] offset:-4096
	global_load_dwordx2 v[224:225], v190, s[46:47]
	v_add_u32_e32 v190, 0x2000, v190
	global_load_dwordx2 v[226:227], v190, s[46:47] offset:-4096
	global_load_dwordx2 v[228:229], v190, s[46:47]
	v_add_u32_e32 v190, 0x2000, v190
	global_load_dwordx2 v[230:231], v190, s[46:47] offset:-4096
	global_load_dwordx2 v[232:233], v190, s[46:47]
	v_xor_b32_e32 v66, 0x80000000, v19
	v_mov_b32_e32 v67, v19
	v_mov_b32_e32 v17, v164
	s_nop 0
	v_pk_mul_f32 v[66:67], v[66:67], v[50:51] op_sel:[0,1] op_sel_hi:[1,0]
	s_nop 0
	v_pk_fma_f32 v[18:19], v[18:19], v[50:51], v[66:67] op_sel_hi:[0,1,1]
	v_mov_b32_e32 v50, v165
	v_mov_b32_e32 v17, v166
	v_mov_b32_e32 v66, v167
	v_mov_b32_e32 v17, v168
	s_nop 0
	v_pk_mul_f32 v[40:41], v[40:41], v[68:69] op_sel_hi:[1,0]
	v_mov_b32_e32 v17, v170
	v_pk_fma_f32 v[22:23], v[22:23], v[50:51], v[40:41] op_sel_hi:[1,0,1]
	v_pk_add_f32 v[40:41], v[24:25], v[42:43]
	v_pk_add_f32 v[24:25], v[24:25], v[42:43] neg_lo:[0,1] neg_hi:[0,1]
	s_nop 0
	v_xor_b32_e32 v42, 0x80000000, v25
	v_mov_b32_e32 v43, v24
	v_pk_mul_f32 v[42:43], v[42:43], v[66:67] op_sel_hi:[1,0]
	v_mov_b32_e32 v17, v171
	v_pk_fma_f32 v[24:25], v[24:25], v[66:67], v[42:43] op_sel_hi:[1,0,1]
	v_pk_add_f32 v[42:43], v[26:27], v[46:47]
	v_pk_add_f32 v[26:27], v[26:27], v[46:47] neg_lo:[0,1] neg_hi:[0,1]
	s_nop 0
	v_pk_mul_f32 v[46:47], v[26:27], v[68:69] op_sel_hi:[1,0]
	v_xor_b32_e32 v72, 0x80000000, v27
	v_mov_b32_e32 v73, v26
	v_pk_fma_f32 v[26:27], v[72:73], v[50:51], v[46:47] op_sel_hi:[1,0,1]
	v_pk_add_f32 v[46:47], v[28:29], v[44:45]
	v_pk_add_f32 v[28:29], v[28:29], v[44:45] neg_lo:[0,1] neg_hi:[0,1]
	v_mov_b32_e32 v17, v175
	v_xor_b32_e32 v44, 0x80000000, v29
	v_mov_b32_e32 v45, v28
	v_pk_add_f32 v[28:29], v[30:31], v[48:49]
	v_pk_add_f32 v[30:31], v[30:31], v[48:49] neg_lo:[0,1] neg_hi:[0,1]
	s_nop 0
	v_pk_mul_f32 v[48:49], v[30:31], v[68:69] op_sel_hi:[1,0] neg_lo:[0,1] neg_hi:[0,1]
	v_xor_b32_e32 v72, 0x80000000, v31
	v_mov_b32_e32 v73, v30
	v_pk_fma_f32 v[30:31], v[72:73], v[50:51], v[48:49] op_sel_hi:[1,0,1]
	v_pk_add_f32 v[48:49], v[32:33], v[38:39]
	v_pk_add_f32 v[32:33], v[32:33], v[38:39] neg_lo:[0,1] neg_hi:[0,1]
	s_nop 0
	v_xor_b32_e32 v38, 0x80000000, v33
	v_mov_b32_e32 v39, v32
	v_pk_mul_f32 v[38:39], v[38:39], v[66:67] op_sel_hi:[1,0]
	s_nop 0
	v_pk_fma_f32 v[32:33], v[32:33], v[66:67], v[38:39] op_sel_hi:[1,0,1] neg_lo:[0,1,0] neg_hi:[0,1,0]
	v_pk_add_f32 v[38:39], v[34:35], v[18:19]
	v_pk_add_f32 v[18:19], v[34:35], v[18:19] neg_lo:[0,1] neg_hi:[0,1]
	s_nop 0
	v_xor_b32_e32 v34, 0x80000000, v19
	v_mov_b32_e32 v35, v18
	v_pk_mul_f32 v[34:35], v[34:35], v[68:69] op_sel_hi:[1,0]
	v_mov_b32_e32 v68, v169
	v_pk_fma_f32 v[18:19], v[18:19], v[50:51], v[34:35] op_sel_hi:[1,0,1] neg_lo:[0,1,0] neg_hi:[0,1,0]
	v_pk_add_f32 v[50:51], v[36:37], v[28:29]
	v_pk_add_f32 v[28:29], v[36:37], v[28:29] neg_lo:[0,1] neg_hi:[0,1]
	v_pk_add_f32 v[34:35], v[70:71], v[46:47]
	v_xor_b32_e32 v36, 0x80000000, v29
	v_mov_b32_e32 v37, v28
	v_pk_mul_f32 v[36:37], v[36:37], v[66:67] op_sel_hi:[1,0]
	v_pk_add_f32 v[46:47], v[70:71], v[46:47] neg_lo:[0,1] neg_hi:[0,1]
	v_pk_fma_f32 v[28:29], v[28:29], v[66:67], v[36:37] op_sel_hi:[1,0,1]
	v_pk_add_f32 v[36:37], v[40:41], v[48:49]
	v_pk_add_f32 v[40:41], v[40:41], v[48:49] neg_lo:[0,1] neg_hi:[0,1]
	s_nop 0
	v_xor_b32_e32 v48, 0x80000000, v41
	v_mov_b32_e32 v49, v40
	v_pk_add_f32 v[40:41], v[42:43], v[38:39]
	v_pk_add_f32 v[38:39], v[42:43], v[38:39] neg_lo:[0,1] neg_hi:[0,1]
	s_nop 0
	v_xor_b32_e32 v42, 0x80000000, v39
	v_mov_b32_e32 v43, v38
	v_pk_mul_f32 v[42:43], v[66:67], v[42:43] op_sel_hi:[0,1]
	v_pk_fma_f32 v[38:39], v[38:39], v[66:67], v[42:43] op_sel_hi:[1,0,1] neg_lo:[0,1,0] neg_hi:[0,1,0]
	v_pk_add_f32 v[42:43], v[34:35], v[36:37]
	v_pk_add_f32 v[34:35], v[34:35], v[36:37] neg_lo:[0,1] neg_hi:[0,1]
	v_pk_add_f32 v[36:37], v[50:51], v[40:41]
	v_pk_add_f32 v[40:41], v[50:51], v[40:41] neg_lo:[0,1] neg_hi:[0,1]
	s_nop 0
	v_xor_b32_e32 v50, 0x80000000, v41
	v_mov_b32_e32 v51, v40
	v_pk_add_f32 v[40:41], v[42:43], v[36:37]
	v_pk_add_f32 v[36:37], v[42:43], v[36:37] neg_lo:[0,1] neg_hi:[0,1]
	v_pk_add_f32 v[42:43], v[34:35], v[50:51]
	v_pk_add_f32 v[34:35], v[34:35], v[50:51] neg_lo:[0,1] neg_hi:[0,1]
	v_pk_add_f32 v[50:51], v[46:47], v[48:49]
	v_pk_add_f32 v[46:47], v[46:47], v[48:49] neg_lo:[0,1] neg_hi:[0,1]
	v_pk_add_f32 v[48:49], v[28:29], v[38:39]
	v_pk_add_f32 v[28:29], v[28:29], v[38:39] neg_lo:[0,1] neg_hi:[0,1]
	s_nop 0
	v_xor_b32_e32 v38, 0x80000000, v29
	v_mov_b32_e32 v39, v28
	v_pk_add_f32 v[28:29], v[50:51], v[48:49]
	v_pk_add_f32 v[48:49], v[50:51], v[48:49] neg_lo:[0,1] neg_hi:[0,1]
	v_pk_add_f32 v[50:51], v[46:47], v[38:39]
	v_pk_add_f32 v[38:39], v[46:47], v[38:39] neg_lo:[0,1] neg_hi:[0,1]
	v_pk_add_f32 v[46:47], v[20:21], v[44:45]
	v_pk_add_f32 v[20:21], v[20:21], v[44:45] neg_lo:[0,1] neg_hi:[0,1]
	v_pk_add_f32 v[44:45], v[22:23], v[30:31]
	v_pk_add_f32 v[22:23], v[22:23], v[30:31] neg_lo:[0,1] neg_hi:[0,1]
	s_nop 0
	v_xor_b32_e32 v30, 0x80000000, v23
	v_mov_b32_e32 v31, v22
	v_pk_mul_f32 v[30:31], v[66:67], v[30:31] op_sel_hi:[0,1]
	v_pk_fma_f32 v[22:23], v[66:67], v[22:23], v[30:31] op_sel_hi:[0,1,1]
	v_pk_add_f32 v[30:31], v[24:25], v[32:33]
	v_pk_add_f32 v[24:25], v[24:25], v[32:33] neg_lo:[0,1] neg_hi:[0,1]
	s_nop 0
	v_xor_b32_e32 v32, 0x80000000, v25
	v_mov_b32_e32 v33, v24
	v_pk_add_f32 v[24:25], v[26:27], v[18:19]
	v_pk_add_f32 v[18:19], v[26:27], v[18:19] neg_lo:[0,1] neg_hi:[0,1]
	s_nop 0
	v_xor_b32_e32 v26, 0x80000000, v19
	v_mov_b32_e32 v27, v18
	v_pk_mul_f32 v[26:27], v[66:67], v[26:27] op_sel_hi:[0,1]
	v_pk_fma_f32 v[18:19], v[66:67], v[18:19], v[26:27] op_sel_hi:[0,1,1] neg_lo:[1,0,0] neg_hi:[1,0,0]
	v_pk_add_f32 v[26:27], v[46:47], v[30:31]
	v_pk_add_f32 v[30:31], v[46:47], v[30:31] neg_lo:[0,1] neg_hi:[0,1]
	v_pk_add_f32 v[46:47], v[44:45], v[24:25]
	v_pk_add_f32 v[24:25], v[44:45], v[24:25] neg_lo:[0,1] neg_hi:[0,1]
	v_mov_b32_e32 v66, v167
	v_xor_b32_e32 v44, 0x80000000, v25
	v_mov_b32_e32 v45, v24
	v_pk_add_f32 v[24:25], v[26:27], v[46:47]
	v_pk_add_f32 v[26:27], v[26:27], v[46:47] neg_lo:[0,1] neg_hi:[0,1]
	v_pk_add_f32 v[46:47], v[30:31], v[44:45]
	v_pk_add_f32 v[30:31], v[30:31], v[44:45] neg_lo:[0,1] neg_hi:[0,1]
	v_pk_add_f32 v[44:45], v[20:21], v[32:33]
	v_pk_add_f32 v[20:21], v[20:21], v[32:33] neg_lo:[0,1] neg_hi:[0,1]
	v_pk_add_f32 v[32:33], v[22:23], v[18:19]
	v_pk_add_f32 v[18:19], v[22:23], v[18:19] neg_lo:[0,1] neg_hi:[0,1]
	s_nop 0
	v_xor_b32_e32 v22, 0x80000000, v19
	v_mov_b32_e32 v23, v18
	v_pk_add_f32 v[18:19], v[44:45], v[32:33]
	v_pk_add_f32 v[32:33], v[44:45], v[32:33] neg_lo:[0,1] neg_hi:[0,1]
	v_pk_add_f32 v[44:45], v[20:21], v[22:23]
	v_pk_add_f32 v[20:21], v[20:21], v[22:23] neg_lo:[0,1] neg_hi:[0,1]
	ds_write_b64 v10, v[40:41]
	ds_write_b64 v13, v[24:25]
	ds_write_b64 v15, v[28:29]
	ds_write_b64 v52, v[18:19]
	ds_write_b64 v53, v[42:43]
	ds_write_b64 v54, v[46:47]
	ds_write_b64 v55, v[50:51]
	ds_write_b64 v56, v[44:45]
	ds_write_b64 v57, v[36:37]
	ds_write_b64 v58, v[26:27]
	ds_write_b64 v59, v[48:49]
	ds_write_b64 v60, v[32:33]
	ds_write_b64 v61, v[34:35]
	ds_write_b64 v62, v[30:31]
	ds_write_b64 v63, v[38:39]
	ds_write_b64 v64, v[20:21]
	v_mov_b32_e32 v10, v177
	v_mov_b32_e32 v64, v165
	v_lshlrev_b32_e32 v13, 3, v17
	v_lshlrev_b32_e32 v48, 3, v10
	v_add3_u32 v10, 0, v13, v48
	v_xor_b32_e32 v13, 1, v17
	v_xor_b32_e32 v34, 8, v17
	v_xor_b32_e32 v36, 9, v17
	v_lshlrev_b32_e32 v13, 3, v13
	v_xor_b32_e32 v15, 2, v17
	v_xor_b32_e32 v24, 3, v17
	v_xor_b32_e32 v26, 4, v17
	v_xor_b32_e32 v28, 5, v17
	v_xor_b32_e32 v30, 6, v17
	v_xor_b32_e32 v32, 7, v17
	v_lshlrev_b32_e32 v34, 3, v34
	v_lshlrev_b32_e32 v36, 3, v36
	v_xor_b32_e32 v38, 10, v17
	v_xor_b32_e32 v40, 11, v17
	v_xor_b32_e32 v42, 12, v17
	v_xor_b32_e32 v44, 13, v17
	v_xor_b32_e32 v46, 14, v17
	v_xor_b32_e32 v17, 15, v17
	v_add3_u32 v13, 0, v13, v48
	v_lshlrev_b32_e32 v15, 3, v15
	v_lshlrev_b32_e32 v24, 3, v24
	v_lshlrev_b32_e32 v26, 3, v26
	v_lshlrev_b32_e32 v28, 3, v28
	v_lshlrev_b32_e32 v30, 3, v30
	v_lshlrev_b32_e32 v32, 3, v32
	v_add3_u32 v55, 0, v34, v48
	v_add3_u32 v56, 0, v36, v48
	v_lshlrev_b32_e32 v38, 3, v38
	v_lshlrev_b32_e32 v40, 3, v40
	v_lshlrev_b32_e32 v42, 3, v42
	v_lshlrev_b32_e32 v44, 3, v44
	v_lshlrev_b32_e32 v46, 3, v46
	v_lshlrev_b32_e32 v17, 3, v17
	ds_read_b64 v[18:19], v10
	ds_read_b64 v[20:21], v13
	v_add3_u32 v15, 0, v15, v48
	v_add3_u32 v50, 0, v24, v48
	v_add3_u32 v51, 0, v26, v48
	v_add3_u32 v52, 0, v28, v48
	v_add3_u32 v53, 0, v30, v48
	v_add3_u32 v54, 0, v32, v48
	ds_read_b64 v[34:35], v55
	ds_read_b64 v[36:37], v56
	v_add3_u32 v57, 0, v38, v48
	v_add3_u32 v58, 0, v40, v48
	v_add3_u32 v59, 0, v42, v48
	v_add3_u32 v60, 0, v44, v48
	v_add3_u32 v61, 0, v46, v48
	v_add3_u32 v62, 0, v17, v48
	v_mov_b32_e32 v17, v1
	ds_read_b64 v[22:23], v15
	ds_read_b64 v[24:25], v50
	ds_read_b64 v[26:27], v51
	ds_read_b64 v[28:29], v52
	ds_read_b64 v[30:31], v53
	ds_read_b64 v[32:33], v54
	ds_read_b64 v[38:39], v57
	ds_read_b64 v[40:41], v58
	ds_read_b64 v[42:43], v59
	ds_read_b64 v[44:45], v60
	ds_read_b64 v[46:47], v61
	ds_read_b64 v[48:49], v62
	s_waitcnt lgkmcnt(13)
	v_pk_add_f32 v[70:71], v[18:19], v[34:35]
	v_mov_b32_e32 v17, v164
	v_pk_add_f32 v[18:19], v[18:19], v[34:35] neg_lo:[0,1] neg_hi:[0,1]
	v_mov_b32_e32 v17, v166
	s_waitcnt lgkmcnt(12)
	v_pk_add_f32 v[34:35], v[20:21], v[36:37]
	v_pk_add_f32 v[20:21], v[20:21], v[36:37] neg_lo:[0,1] neg_hi:[0,1]
	v_mov_b32_e32 v17, v168
	v_xor_b32_e32 v36, 0x80000000, v21
	v_mov_b32_e32 v37, v20
	s_nop 0
	v_pk_mul_f32 v[36:37], v[36:37], v[68:69] op_sel_hi:[1,0] neg_lo:[0,1] neg_hi:[0,1]
	v_mov_b32_e32 v17, v170
	v_pk_fma_f32 v[20:21], v[20:21], v[64:65], v[36:37] op_sel_hi:[1,0,1]
	s_waitcnt lgkmcnt(5)
	v_pk_add_f32 v[36:37], v[22:23], v[38:39]
	v_pk_add_f32 v[22:23], v[22:23], v[38:39] neg_lo:[0,1] neg_hi:[0,1]
	s_nop 0
	v_xor_b32_e32 v38, 0x80000000, v23
	v_mov_b32_e32 v39, v22
	v_pk_mul_f32 v[38:39], v[38:39], v[66:67] op_sel_hi:[1,0] neg_lo:[0,1] neg_hi:[0,1]
	v_mov_b32_e32 v17, v171
	v_pk_fma_f32 v[22:23], v[22:23], v[66:67], v[38:39] op_sel_hi:[1,0,1]
	s_waitcnt lgkmcnt(4)
	v_pk_add_f32 v[38:39], v[24:25], v[40:41]
	v_pk_add_f32 v[24:25], v[24:25], v[40:41] neg_lo:[0,1] neg_hi:[0,1]
	s_nop 0
	v_pk_mul_f32 v[40:41], v[24:25], v[68:69] op_sel_hi:[1,0]
	v_xor_b32_e32 v72, 0x80000000, v25
	v_mov_b32_e32 v73, v24
	v_pk_fma_f32 v[24:25], v[72:73], v[64:65], v[40:41] op_sel_hi:[1,0,1] neg_lo:[0,1,0] neg_hi:[0,1,0]
	s_waitcnt lgkmcnt(3)
	v_pk_add_f32 v[40:41], v[26:27], v[42:43]
	v_pk_add_f32 v[26:27], v[26:27], v[42:43] neg_lo:[0,1] neg_hi:[0,1]
	s_nop 0
	v_xor_b32_e32 v73, 0x80000000, v26
	v_mov_b32_e32 v72, v27
	s_waitcnt lgkmcnt(2)
	v_pk_add_f32 v[26:27], v[28:29], v[44:45]
	v_pk_add_f32 v[28:29], v[28:29], v[44:45] neg_lo:[0,1] neg_hi:[0,1]
	s_nop 0
	v_pk_mul_f32 v[42:43], v[28:29], v[68:69] op_sel_hi:[1,0] neg_lo:[0,1] neg_hi:[0,1]
	v_xor_b32_e32 v44, 0x80000000, v29
	v_mov_b32_e32 v45, v28
	v_pk_fma_f32 v[28:29], v[44:45], v[64:65], v[42:43] op_sel_hi:[1,0,1] neg_lo:[0,1,0] neg_hi:[0,1,0]
	s_waitcnt lgkmcnt(1)
	v_pk_add_f32 v[42:43], v[30:31], v[46:47]
	v_pk_add_f32 v[30:31], v[30:31], v[46:47] neg_lo:[0,1] neg_hi:[0,1]
	s_nop 0
	v_xor_b32_e32 v44, 0x80000000, v31
	v_mov_b32_e32 v45, v30
	v_pk_mul_f32 v[44:45], v[44:45], v[66:67] op_sel_hi:[1,0] neg_lo:[0,1] neg_hi:[0,1]
	s_nop 0
	v_pk_fma_f32 v[30:31], v[30:31], v[66:67], v[44:45] op_sel_hi:[1,0,1] neg_lo:[0,1,0] neg_hi:[0,1,0]
	s_waitcnt lgkmcnt(0)
	v_pk_add_f32 v[44:45], v[32:33], v[48:49]
	v_pk_add_f32 v[32:33], v[32:33], v[48:49] neg_lo:[0,1] neg_hi:[0,1]
	v_pk_add_f32 v[48:49], v[34:35], v[26:27]
	v_pk_add_f32 v[26:27], v[34:35], v[26:27] neg_lo:[0,1] neg_hi:[0,1]
	v_xor_b32_e32 v46, 0x80000000, v33
	v_xor_b32_e32 v34, 0x80000000, v27
	v_mov_b32_e32 v35, v26
	v_pk_mul_f32 v[34:35], v[34:35], v[66:67] op_sel_hi:[1,0] neg_lo:[0,1] neg_hi:[0,1]
	v_mov_b32_e32 v47, v32
	v_pk_fma_f32 v[26:27], v[26:27], v[66:67], v[34:35] op_sel_hi:[1,0,1]
	v_pk_add_f32 v[34:35], v[36:37], v[42:43]
	v_pk_add_f32 v[36:37], v[36:37], v[42:43] neg_lo:[0,1] neg_hi:[0,1]
	v_pk_mul_f32 v[46:47], v[46:47], v[68:69] op_sel_hi:[1,0] neg_lo:[0,1] neg_hi:[0,1]
	v_xor_b32_e32 v43, 0x80000000, v36
	v_mov_b32_e32 v42, v37
	v_pk_add_f32 v[36:37], v[38:39], v[44:45]
	v_pk_add_f32 v[38:39], v[38:39], v[44:45] neg_lo:[0,1] neg_hi:[0,1]
	v_pk_fma_f32 v[46:47], v[32:33], v[64:65], v[46:47] op_sel_hi:[1,0,1] neg_lo:[0,1,0] neg_hi:[0,1,0]
	v_xor_b32_e32 v44, 0x80000000, v39
	v_mov_b32_e32 v45, v38
	v_pk_add_f32 v[32:33], v[70:71], v[40:41]
	v_pk_mul_f32 v[44:45], v[44:45], v[66:67] op_sel_hi:[1,0] neg_lo:[0,1] neg_hi:[0,1]
	v_pk_add_f32 v[40:41], v[70:71], v[40:41] neg_lo:[0,1] neg_hi:[0,1]
	v_pk_fma_f32 v[38:39], v[38:39], v[66:67], v[44:45] op_sel_hi:[1,0,1] neg_lo:[0,1,0] neg_hi:[0,1,0]
	v_pk_add_f32 v[44:45], v[32:33], v[34:35]
	v_pk_add_f32 v[32:33], v[32:33], v[34:35] neg_lo:[0,1] neg_hi:[0,1]
	v_pk_add_f32 v[34:35], v[48:49], v[36:37]
	v_pk_add_f32 v[36:37], v[48:49], v[36:37] neg_lo:[0,1] neg_hi:[0,1]
	v_pk_add_f32 v[64:65], v[44:45], v[34:35]
	v_xor_b32_e32 v49, 0x80000000, v36
	v_mov_b32_e32 v48, v37
	v_pk_add_f32 v[36:37], v[44:45], v[34:35] neg_lo:[0,1] neg_hi:[0,1]
	v_pk_add_f32 v[68:69], v[32:33], v[48:49]
	v_pk_add_f32 v[44:45], v[32:33], v[48:49] neg_lo:[0,1] neg_hi:[0,1]
	v_pk_add_f32 v[32:33], v[40:41], v[42:43]
	v_pk_add_f32 v[34:35], v[40:41], v[42:43] neg_lo:[0,1] neg_hi:[0,1]
	v_pk_add_f32 v[40:41], v[26:27], v[38:39]
	v_pk_add_f32 v[26:27], v[26:27], v[38:39] neg_lo:[0,1] neg_hi:[0,1]
	v_pk_add_f32 v[42:43], v[32:33], v[40:41] neg_lo:[0,1] neg_hi:[0,1]
	v_xor_b32_e32 v39, 0x80000000, v26
	v_mov_b32_e32 v38, v27
	v_pk_add_f32 v[26:27], v[32:33], v[40:41]
	v_pk_add_f32 v[40:41], v[20:21], v[28:29]
	v_pk_add_f32 v[20:21], v[20:21], v[28:29] neg_lo:[0,1] neg_hi:[0,1]
	v_pk_add_f32 v[32:33], v[34:35], v[38:39]
	v_xor_b32_e32 v28, 0x80000000, v21
	v_mov_b32_e32 v29, v20
	v_pk_mul_f32 v[28:29], v[66:67], v[28:29] op_sel_hi:[0,1] neg_lo:[1,0] neg_hi:[1,0]
	v_pk_fma_f32 v[20:21], v[66:67], v[20:21], v[28:29] op_sel_hi:[0,1,1]
	v_pk_add_f32 v[28:29], v[22:23], v[30:31]
	v_pk_add_f32 v[22:23], v[22:23], v[30:31] neg_lo:[0,1] neg_hi:[0,1]
	v_pk_add_f32 v[38:39], v[34:35], v[38:39] neg_lo:[0,1] neg_hi:[0,1]
	v_xor_b32_e32 v31, 0x80000000, v22
	v_mov_b32_e32 v30, v23
	v_pk_add_f32 v[22:23], v[24:25], v[46:47]
	v_pk_add_f32 v[24:25], v[24:25], v[46:47] neg_lo:[0,1] neg_hi:[0,1]
	v_pk_add_f32 v[34:35], v[18:19], v[72:73]
	v_xor_b32_e32 v46, 0x80000000, v25
	v_mov_b32_e32 v47, v24
	v_pk_mul_f32 v[46:47], v[66:67], v[46:47] op_sel_hi:[0,1] neg_lo:[1,0] neg_hi:[1,0]
	v_pk_fma_f32 v[24:25], v[66:67], v[24:25], v[46:47] op_sel_hi:[0,1,1] neg_lo:[1,0,0] neg_hi:[1,0,0]
	v_pk_add_f32 v[46:47], v[34:35], v[28:29]
	v_pk_add_f32 v[28:29], v[34:35], v[28:29] neg_lo:[0,1] neg_hi:[0,1]
	v_pk_add_f32 v[34:35], v[40:41], v[22:23]
	v_pk_add_f32 v[22:23], v[40:41], v[22:23] neg_lo:[0,1] neg_hi:[0,1]
	v_pk_add_f32 v[18:19], v[18:19], v[72:73] neg_lo:[0,1] neg_hi:[0,1]
	v_xor_b32_e32 v49, 0x80000000, v22
	v_mov_b32_e32 v48, v23
	v_pk_add_f32 v[66:67], v[28:29], v[48:49]
	v_pk_add_f32 v[48:49], v[28:29], v[48:49] neg_lo:[0,1] neg_hi:[0,1]
	v_pk_add_f32 v[28:29], v[18:19], v[30:31]
	v_pk_add_f32 v[18:19], v[18:19], v[30:31] neg_lo:[0,1] neg_hi:[0,1]
	v_pk_add_f32 v[30:31], v[20:21], v[24:25]
	v_pk_add_f32 v[20:21], v[20:21], v[24:25] neg_lo:[0,1] neg_hi:[0,1]
	v_pk_add_f32 v[22:23], v[46:47], v[34:35]
	v_xor_b32_e32 v25, 0x80000000, v20
	v_add_u32_e32 v20, 0x2000, v16
	v_mov_b32_e32 v24, v21
	v_ashrrev_i32_e32 v21, 31, v20
	v_lshl_add_u64 v[20:21], v[20:21], 3, s[46:47]
	s_waitcnt vmcnt(0)
	v_mov_b32_e32 v20, v202
	v_mov_b32_e32 v21, v203
	v_pk_add_f32 v[40:41], v[46:47], v[34:35] neg_lo:[0,1] neg_hi:[0,1]
	v_pk_add_f32 v[34:35], v[18:19], v[24:25]
	v_pk_add_f32 v[18:19], v[18:19], v[24:25] neg_lo:[0,1] neg_hi:[0,1]
	v_xor_b32_e32 v24, 0x80000000, v65
	v_mov_b32_e32 v25, v65
	v_pk_add_f32 v[70:71], v[28:29], v[30:31]
	v_pk_add_f32 v[46:47], v[28:29], v[30:31] neg_lo:[0,1] neg_hi:[0,1]
	v_xor_b32_e32 v28, 0x80000000, v23
	v_mov_b32_e32 v29, v23
	v_xor_b32_e32 v30, 0x80000000, v69
	v_mov_b32_e32 v31, v69
	s_nop 0
	v_pk_mul_f32 v[24:25], v[24:25], v[20:21] op_sel:[0,1] op_sel_hi:[1,0]
	s_nop 0
	v_pk_fma_f32 v[20:21], v[64:65], v[20:21], v[24:25] op_sel_hi:[0,1,1]
	v_add_u32_e32 v24, 0x2200, v16
	v_ashrrev_i32_e32 v25, 31, v24
	v_lshl_add_u64 v[24:25], v[24:25], 3, s[46:47]
	v_mov_b32_e32 v24, v204
	v_mov_b32_e32 v25, v205
	v_xor_b32_e32 v64, 0x80000000, v67
	v_mov_b32_e32 v65, v67
	s_nop 0
	v_pk_mul_f32 v[28:29], v[24:25], v[28:29] op_sel:[1,0] op_sel_hi:[0,1]
	v_pk_fma_f32 v[22:23], v[24:25], v[22:23], v[28:29] op_sel_hi:[1,0,1]
	v_add_u32_e32 v24, 0x2400, v16
	v_ashrrev_i32_e32 v25, 31, v24
	v_lshl_add_u64 v[24:25], v[24:25], 3, s[46:47]
	v_mov_b32_e32 v24, v206
	v_mov_b32_e32 v25, v207
	v_xor_b32_e32 v28, 0x80000000, v27
	v_mov_b32_e32 v29, v27
	s_nop 0
	v_pk_mul_f32 v[28:29], v[28:29], v[24:25] op_sel:[0,1] op_sel_hi:[1,0]
	s_nop 0
	v_pk_fma_f32 v[24:25], v[26:27], v[24:25], v[28:29] op_sel_hi:[0,1,1]
	v_add_u32_e32 v26, 0x2600, v16
	v_ashrrev_i32_e32 v27, 31, v26
	v_lshl_add_u64 v[26:27], v[26:27], 3, s[46:47]
	v_mov_b32_e32 v26, v208
	v_mov_b32_e32 v27, v209
	v_xor_b32_e32 v28, 0x80000000, v71
	v_mov_b32_e32 v29, v71
	s_nop 0
	v_pk_mul_f32 v[28:29], v[26:27], v[28:29] op_sel:[1,0] op_sel_hi:[0,1]
	v_pk_fma_f32 v[26:27], v[26:27], v[70:71], v[28:29] op_sel_hi:[1,0,1]
	v_add_u32_e32 v28, 0x2800, v16
	v_ashrrev_i32_e32 v29, 31, v28
	v_lshl_add_u64 v[28:29], v[28:29], 3, s[46:47]
	v_mov_b32_e32 v28, v210
	v_mov_b32_e32 v29, v211
	s_nop 0
	v_pk_mul_f32 v[30:31], v[30:31], v[28:29] op_sel:[0,1] op_sel_hi:[1,0]
	s_nop 0
	v_pk_fma_f32 v[28:29], v[68:69], v[28:29], v[30:31] op_sel_hi:[0,1,1]
	v_add_u32_e32 v30, 0x2a00, v16
	v_ashrrev_i32_e32 v31, 31, v30
	v_lshl_add_u64 v[30:31], v[30:31], 3, s[46:47]
	v_mov_b32_e32 v30, v212
	v_mov_b32_e32 v31, v213
	s_nop 0
	v_pk_mul_f32 v[64:65], v[30:31], v[64:65] op_sel:[1,0] op_sel_hi:[0,1]
	v_pk_fma_f32 v[30:31], v[30:31], v[66:67], v[64:65] op_sel_hi:[1,0,1]
	v_add_u32_e32 v64, 0x2c00, v16
	v_ashrrev_i32_e32 v65, 31, v64
	v_lshl_add_u64 v[64:65], v[64:65], 3, s[46:47]
	v_mov_b32_e32 v64, v214
	v_mov_b32_e32 v65, v215
	v_xor_b32_e32 v66, 0x80000000, v33
	v_mov_b32_e32 v67, v33
	s_nop 0
	v_pk_mul_f32 v[66:67], v[66:67], v[64:65] op_sel:[0,1] op_sel_hi:[1,0]
	s_nop 0
	v_pk_fma_f32 v[32:33], v[32:33], v[64:65], v[66:67] op_sel_hi:[0,1,1]
	v_add_u32_e32 v64, 0x2e00, v16
	v_ashrrev_i32_e32 v65, 31, v64
	v_lshl_add_u64 v[64:65], v[64:65], 3, s[46:47]
	v_mov_b32_e32 v64, v216
	v_mov_b32_e32 v65, v217
	v_xor_b32_e32 v66, 0x80000000, v35
	v_mov_b32_e32 v67, v35
	s_nop 0
	v_pk_mul_f32 v[66:67], v[64:65], v[66:67] op_sel:[1,0] op_sel_hi:[0,1]
	v_pk_fma_f32 v[34:35], v[64:65], v[34:35], v[66:67] op_sel_hi:[1,0,1]
	v_add_u32_e32 v64, 0x3000, v16
	v_ashrrev_i32_e32 v65, 31, v64
	v_lshl_add_u64 v[64:65], v[64:65], 3, s[46:47]
	v_mov_b32_e32 v64, v218
	v_mov_b32_e32 v65, v219
	v_xor_b32_e32 v66, 0x80000000, v37
	v_mov_b32_e32 v67, v37
	s_nop 0
	v_pk_mul_f32 v[66:67], v[66:67], v[64:65] op_sel:[0,1] op_sel_hi:[1,0]
	s_nop 0
	v_pk_fma_f32 v[36:37], v[36:37], v[64:65], v[66:67] op_sel_hi:[0,1,1]
	v_add_u32_e32 v64, 0x3200, v16
	v_ashrrev_i32_e32 v65, 31, v64
	v_lshl_add_u64 v[64:65], v[64:65], 3, s[46:47]
	v_mov_b32_e32 v64, v220
	v_mov_b32_e32 v65, v221
	v_xor_b32_e32 v66, 0x80000000, v41
	v_mov_b32_e32 v67, v41
	v_pk_add_f32 v[68:69], v[20:21], v[36:37]
	v_pk_add_f32 v[20:21], v[20:21], v[36:37] neg_lo:[0,1] neg_hi:[0,1]
	s_nop 0
	v_pk_mul_f32 v[66:67], v[66:67], v[64:65] op_sel:[0,1] op_sel_hi:[1,0]
	s_nop 0
	v_pk_fma_f32 v[40:41], v[40:41], v[64:65], v[66:67] op_sel_hi:[0,1,1]
	v_add_u32_e32 v64, 0x3400, v16
	v_ashrrev_i32_e32 v65, 31, v64
	v_lshl_add_u64 v[64:65], v[64:65], 3, s[46:47]
	v_mov_b32_e32 v64, v222
	v_mov_b32_e32 v65, v223
	v_xor_b32_e32 v66, 0x80000000, v43
	v_mov_b32_e32 v67, v43
	v_pk_add_f32 v[36:37], v[22:23], v[40:41]
	v_pk_add_f32 v[22:23], v[22:23], v[40:41] neg_lo:[0,1] neg_hi:[0,1]
	s_nop 0
	v_pk_mul_f32 v[66:67], v[66:67], v[64:65] op_sel:[0,1] op_sel_hi:[1,0]
	s_nop 0
	v_pk_fma_f32 v[42:43], v[42:43], v[64:65], v[66:67] op_sel_hi:[0,1,1]
	v_add_u32_e32 v64, 0x3600, v16
	v_ashrrev_i32_e32 v65, 31, v64
	v_lshl_add_u64 v[64:65], v[64:65], 3, s[46:47]
	v_mov_b32_e32 v64, v224
	v_mov_b32_e32 v65, v225
	v_xor_b32_e32 v66, 0x80000000, v47
	v_mov_b32_e32 v67, v47
	v_xor_b32_e32 v40, 0x80000000, v23
	v_mov_b32_e32 v41, v22
	s_nop 0
	v_pk_mul_f32 v[66:67], v[66:67], v[64:65] op_sel:[0,1] op_sel_hi:[1,0]
	s_nop 0
	v_pk_fma_f32 v[46:47], v[46:47], v[64:65], v[66:67] op_sel_hi:[0,1,1]
	v_add_u32_e32 v64, 0x3800, v16
	v_ashrrev_i32_e32 v65, 31, v64
	v_lshl_add_u64 v[64:65], v[64:65], 3, s[46:47]
	v_mov_b32_e32 v64, v226
	v_mov_b32_e32 v65, v227
	v_xor_b32_e32 v66, 0x80000000, v45
	v_mov_b32_e32 v67, v45
	s_nop 0
	v_pk_mul_f32 v[66:67], v[66:67], v[64:65] op_sel:[0,1] op_sel_hi:[1,0]
	s_nop 0
	v_pk_fma_f32 v[44:45], v[44:45], v[64:65], v[66:67] op_sel_hi:[0,1,1]
	v_add_u32_e32 v64, 0x3a00, v16
	v_ashrrev_i32_e32 v65, 31, v64
	v_lshl_add_u64 v[64:65], v[64:65], 3, s[46:47]
	v_mov_b32_e32 v64, v228
	v_mov_b32_e32 v65, v229
	v_xor_b32_e32 v66, 0x80000000, v49
	v_mov_b32_e32 v67, v49
	s_nop 0
	v_pk_mul_f32 v[66:67], v[66:67], v[64:65] op_sel:[0,1] op_sel_hi:[1,0]
	s_nop 0
	v_pk_fma_f32 v[48:49], v[48:49], v[64:65], v[66:67] op_sel_hi:[0,1,1]
	v_add_u32_e32 v64, 0x3c00, v16
	v_ashrrev_i32_e32 v65, 31, v64
	v_lshl_add_u64 v[64:65], v[64:65], 3, s[46:47]
	v_add_u32_e32 v16, 0x3e00, v16
	v_mov_b32_e32 v64, v230
	v_mov_b32_e32 v65, v231
	v_ashrrev_i32_e32 v17, 31, v16
	v_lshl_add_u64 v[16:17], v[16:17], 3, s[46:47]
	v_mov_b32_e32 v16, v232
	v_mov_b32_e32 v17, v233
	v_xor_b32_e32 v66, 0x80000000, v39
	v_mov_b32_e32 v67, v39
	s_nop 0
	v_pk_mul_f32 v[66:67], v[66:67], v[64:65] op_sel:[0,1] op_sel_hi:[1,0]
	s_nop 0
	v_pk_fma_f32 v[38:39], v[38:39], v[64:65], v[66:67] op_sel_hi:[0,1,1]
	v_xor_b32_e32 v64, 0x80000000, v19
	v_mov_b32_e32 v65, v19
	s_nop 0
	v_pk_mul_f32 v[64:65], v[64:65], v[16:17] op_sel:[0,1] op_sel_hi:[1,0]
	v_mov_b32_e32 v66, v169
	v_pk_fma_f32 v[16:17], v[18:19], v[16:17], v[64:65] op_sel_hi:[0,1,1]
	v_mov_b32_e32 v18, v1
	v_mov_b32_e32 v19, v166
	v_mov_b32_e32 v18, v164
	v_mov_b32_e32 v64, v167
	v_mov_b32_e32 v18, v165
	s_nop 0
	v_mov_b32_e32 v19, v168
	s_nop 0
	v_mov_b32_e32 v19, v170
	v_pk_mul_f32 v[40:41], v[40:41], v[66:67] op_sel_hi:[1,0]
	v_mov_b32_e32 v19, v171
	s_nop 0
	v_pk_fma_f32 v[22:23], v[22:23], v[18:19], v[40:41] op_sel_hi:[1,0,1]
	v_pk_add_f32 v[40:41], v[24:25], v[42:43]
	v_pk_add_f32 v[24:25], v[24:25], v[42:43] neg_lo:[0,1] neg_hi:[0,1]
	s_nop 0
	v_xor_b32_e32 v42, 0x80000000, v25
	v_mov_b32_e32 v43, v24
	v_pk_mul_f32 v[42:43], v[42:43], v[64:65] op_sel_hi:[1,0]
	s_nop 0
	v_pk_fma_f32 v[24:25], v[24:25], v[64:65], v[42:43] op_sel_hi:[1,0,1]
	v_pk_add_f32 v[42:43], v[26:27], v[46:47]
	v_pk_add_f32 v[26:27], v[26:27], v[46:47] neg_lo:[0,1] neg_hi:[0,1]
	s_nop 0
	v_pk_mul_f32 v[46:47], v[26:27], v[66:67] op_sel_hi:[1,0]
	v_xor_b32_e32 v70, 0x80000000, v27
	v_mov_b32_e32 v71, v26
	v_pk_fma_f32 v[26:27], v[70:71], v[18:19], v[46:47] op_sel_hi:[1,0,1]
	v_pk_add_f32 v[46:47], v[28:29], v[44:45]
	v_pk_add_f32 v[28:29], v[28:29], v[44:45] neg_lo:[0,1] neg_hi:[0,1]
	s_nop 0
	v_xor_b32_e32 v44, 0x80000000, v29
	v_mov_b32_e32 v45, v28
	v_pk_add_f32 v[28:29], v[30:31], v[48:49]
	v_pk_add_f32 v[30:31], v[30:31], v[48:49] neg_lo:[0,1] neg_hi:[0,1]
	s_nop 0
	v_pk_mul_f32 v[48:49], v[30:31], v[66:67] op_sel_hi:[1,0] neg_lo:[0,1] neg_hi:[0,1]
	v_xor_b32_e32 v70, 0x80000000, v31
	v_mov_b32_e32 v71, v30
	v_pk_fma_f32 v[30:31], v[70:71], v[18:19], v[48:49] op_sel_hi:[1,0,1]
	v_pk_add_f32 v[48:49], v[32:33], v[38:39]
	v_pk_add_f32 v[32:33], v[32:33], v[38:39] neg_lo:[0,1] neg_hi:[0,1]
	s_nop 0
	v_xor_b32_e32 v38, 0x80000000, v33
	v_mov_b32_e32 v39, v32
	v_pk_mul_f32 v[38:39], v[38:39], v[64:65] op_sel_hi:[1,0]
	s_nop 0
	v_pk_fma_f32 v[32:33], v[32:33], v[64:65], v[38:39] op_sel_hi:[1,0,1] neg_lo:[0,1,0] neg_hi:[0,1,0]
	v_pk_add_f32 v[38:39], v[34:35], v[16:17]
	v_pk_add_f32 v[16:17], v[34:35], v[16:17] neg_lo:[0,1] neg_hi:[0,1]
	s_nop 0
	v_xor_b32_e32 v34, 0x80000000, v17
	v_mov_b32_e32 v35, v16
	v_pk_mul_f32 v[34:35], v[34:35], v[66:67] op_sel_hi:[1,0]
	s_nop 0
	v_pk_fma_f32 v[16:17], v[16:17], v[18:19], v[34:35] op_sel_hi:[1,0,1] neg_lo:[0,1,0] neg_hi:[0,1,0]
	v_pk_add_f32 v[18:19], v[68:69], v[46:47]
	v_pk_add_f32 v[34:35], v[68:69], v[46:47] neg_lo:[0,1] neg_hi:[0,1]
	v_pk_add_f32 v[46:47], v[36:37], v[28:29]
	v_pk_add_f32 v[28:29], v[36:37], v[28:29] neg_lo:[0,1] neg_hi:[0,1]
	s_nop 0
	v_xor_b32_e32 v36, 0x80000000, v29
	v_mov_b32_e32 v37, v28
	v_pk_mul_f32 v[36:37], v[36:37], v[64:65] op_sel_hi:[1,0]
	s_nop 0
	v_pk_fma_f32 v[28:29], v[28:29], v[64:65], v[36:37] op_sel_hi:[1,0,1]
	v_pk_add_f32 v[36:37], v[40:41], v[48:49]
	v_pk_add_f32 v[40:41], v[40:41], v[48:49] neg_lo:[0,1] neg_hi:[0,1]
	s_nop 0
	v_xor_b32_e32 v48, 0x80000000, v41
	v_mov_b32_e32 v49, v40
	v_pk_add_f32 v[40:41], v[42:43], v[38:39]
	v_pk_add_f32 v[38:39], v[42:43], v[38:39] neg_lo:[0,1] neg_hi:[0,1]
	s_nop 0
	v_xor_b32_e32 v42, 0x80000000, v39
	v_mov_b32_e32 v43, v38
	v_pk_mul_f32 v[42:43], v[64:65], v[42:43] op_sel_hi:[0,1]
	v_pk_fma_f32 v[38:39], v[38:39], v[64:65], v[42:43] op_sel_hi:[1,0,1] neg_lo:[0,1,0] neg_hi:[0,1,0]
	v_pk_add_f32 v[42:43], v[18:19], v[36:37]
	v_pk_add_f32 v[18:19], v[18:19], v[36:37] neg_lo:[0,1] neg_hi:[0,1]
	v_pk_add_f32 v[36:37], v[46:47], v[40:41]
	v_pk_add_f32 v[40:41], v[46:47], v[40:41] neg_lo:[0,1] neg_hi:[0,1]
	s_nop 0
	v_xor_b32_e32 v46, 0x80000000, v41
	v_mov_b32_e32 v47, v40
	v_pk_add_f32 v[40:41], v[42:43], v[36:37]
	v_pk_add_f32 v[36:37], v[42:43], v[36:37] neg_lo:[0,1] neg_hi:[0,1]
	v_pk_add_f32 v[42:43], v[18:19], v[46:47]
	v_pk_add_f32 v[18:19], v[18:19], v[46:47] neg_lo:[0,1] neg_hi:[0,1]
	v_pk_add_f32 v[46:47], v[34:35], v[48:49]
	v_pk_add_f32 v[34:35], v[34:35], v[48:49] neg_lo:[0,1] neg_hi:[0,1]
	v_pk_add_f32 v[48:49], v[28:29], v[38:39]
	v_pk_add_f32 v[28:29], v[28:29], v[38:39] neg_lo:[0,1] neg_hi:[0,1]
	s_nop 0
	v_xor_b32_e32 v38, 0x80000000, v29
	v_mov_b32_e32 v39, v28
	v_pk_add_f32 v[28:29], v[46:47], v[48:49]
	v_pk_add_f32 v[46:47], v[46:47], v[48:49] neg_lo:[0,1] neg_hi:[0,1]
	v_pk_add_f32 v[48:49], v[34:35], v[38:39]
	v_pk_add_f32 v[34:35], v[34:35], v[38:39] neg_lo:[0,1] neg_hi:[0,1]
	v_pk_add_f32 v[38:39], v[20:21], v[44:45]
	v_pk_add_f32 v[20:21], v[20:21], v[44:45] neg_lo:[0,1] neg_hi:[0,1]
	v_pk_add_f32 v[44:45], v[22:23], v[30:31]
	v_pk_add_f32 v[22:23], v[22:23], v[30:31] neg_lo:[0,1] neg_hi:[0,1]
	s_nop 0
	v_xor_b32_e32 v30, 0x80000000, v23
	v_mov_b32_e32 v31, v22
	v_pk_mul_f32 v[30:31], v[64:65], v[30:31] op_sel_hi:[0,1]
	v_pk_fma_f32 v[22:23], v[64:65], v[22:23], v[30:31] op_sel_hi:[0,1,1]
	v_pk_add_f32 v[30:31], v[24:25], v[32:33]
	v_pk_add_f32 v[24:25], v[24:25], v[32:33] neg_lo:[0,1] neg_hi:[0,1]
	s_nop 0
	v_xor_b32_e32 v32, 0x80000000, v25
	v_mov_b32_e32 v33, v24
	v_pk_add_f32 v[24:25], v[26:27], v[16:17]
	v_pk_add_f32 v[16:17], v[26:27], v[16:17] neg_lo:[0,1] neg_hi:[0,1]
	s_nop 0
	v_xor_b32_e32 v26, 0x80000000, v17
	v_mov_b32_e32 v27, v16
	v_pk_mul_f32 v[26:27], v[64:65], v[26:27] op_sel_hi:[0,1]
	v_pk_fma_f32 v[16:17], v[64:65], v[16:17], v[26:27] op_sel_hi:[0,1,1] neg_lo:[1,0,0] neg_hi:[1,0,0]
	v_pk_add_f32 v[26:27], v[38:39], v[30:31]
	v_pk_add_f32 v[30:31], v[38:39], v[30:31] neg_lo:[0,1] neg_hi:[0,1]
	v_pk_add_f32 v[38:39], v[44:45], v[24:25]
	v_pk_add_f32 v[24:25], v[44:45], v[24:25] neg_lo:[0,1] neg_hi:[0,1]
	s_nop 0
	v_xor_b32_e32 v44, 0x80000000, v25
	v_mov_b32_e32 v45, v24
	v_pk_add_f32 v[24:25], v[26:27], v[38:39]
	v_pk_add_f32 v[26:27], v[26:27], v[38:39] neg_lo:[0,1] neg_hi:[0,1]
	v_pk_add_f32 v[38:39], v[30:31], v[44:45]
	v_pk_add_f32 v[30:31], v[30:31], v[44:45] neg_lo:[0,1] neg_hi:[0,1]
	v_pk_add_f32 v[44:45], v[20:21], v[32:33]
	v_pk_add_f32 v[20:21], v[20:21], v[32:33] neg_lo:[0,1] neg_hi:[0,1]
	v_pk_add_f32 v[32:33], v[22:23], v[16:17]
	v_pk_add_f32 v[16:17], v[22:23], v[16:17] neg_lo:[0,1] neg_hi:[0,1]
	s_nop 0
	v_xor_b32_e32 v22, 0x80000000, v17
	v_mov_b32_e32 v23, v16
	v_pk_add_f32 v[16:17], v[44:45], v[32:33]
	v_pk_add_f32 v[32:33], v[44:45], v[32:33] neg_lo:[0,1] neg_hi:[0,1]
	v_pk_add_f32 v[44:45], v[20:21], v[22:23]
	v_pk_add_f32 v[20:21], v[20:21], v[22:23] neg_lo:[0,1] neg_hi:[0,1]
	ds_write_b64 v10, v[40:41]
	ds_write_b64 v13, v[24:25]
	ds_write_b64 v15, v[28:29]
	ds_write_b64 v50, v[16:17]
	ds_write_b64 v51, v[42:43]
	ds_write_b64 v52, v[38:39]
	ds_write_b64 v53, v[48:49]
	ds_write_b64 v54, v[44:45]
	ds_write_b64 v55, v[36:37]
	ds_write_b64 v56, v[26:27]
	ds_write_b64 v57, v[46:47]
	ds_write_b64 v58, v[32:33]
	ds_write_b64 v59, v[18:19]
	ds_write_b64 v60, v[30:31]
	ds_write_b64 v61, v[34:35]
	ds_write_b64 v62, v[20:21]
	v_mov_b32_e32 v10, v174
	v_mov_b32_e32 v50, v172
	s_waitcnt lgkmcnt(0)
	s_barrier
	v_mov_b32_e32 v20, v180
	v_add_u32_e32 v13, v50, v10
	v_mov_b32_e32 v21, v181
	v_lshl_add_u32 v13, v13, 3, 0
	ds_read2_b64 v[16:19], v13 offset1:16
	v_xad_u32 v15, v50, 1, v10
	v_lshl_add_u32 v15, v15, 3, 0
	s_waitcnt lgkmcnt(0)
	v_xor_b32_e32 v23, 0x80000000, v16
	v_mov_b32_e32 v22, v17
	v_pk_fma_f32 v[16:17], v[22:23], 0, v[16:17] op_sel_hi:[1,0,1]
	v_pk_fma_f32 v[22:23], v[20:21], s[90:91], v[20:21] op_sel:[1,0,0] op_sel_hi:[0,1,1]
	v_xor_b32_e32 v25, 0x80000000, v18
	v_mov_b32_e32 v24, v19
	v_pk_mul_f32 v[24:25], v[22:23], v[24:25] op_sel:[1,0]
	s_nop 0
	v_pk_fma_f32 v[18:19], v[18:19], v[22:23], v[24:25] op_sel_hi:[1,0,1]
	v_xor_b32_e32 v24, 0x80000000, v23
	v_mov_b32_e32 v25, v23
	v_pk_mul_f32 v[24:25], v[20:21], v[24:25] op_sel:[1,0] op_sel_hi:[0,1]
	v_pk_fma_f32 v[26:27], v[20:21], v[22:23], v[24:25] op_sel_hi:[1,0,1]
	ds_read2_b64 v[22:25], v15 offset0:32 offset1:48
	s_waitcnt lgkmcnt(0)
	v_xor_b32_e32 v29, 0x80000000, v22
	v_mov_b32_e32 v28, v23
	v_pk_mul_f32 v[28:29], v[28:29], v[26:27] op_sel:[0,1]
	s_nop 0
	v_pk_fma_f32 v[22:23], v[22:23], v[26:27], v[28:29] op_sel_hi:[1,0,1]
	v_xor_b32_e32 v28, 0x80000000, v27
	v_mov_b32_e32 v29, v27
	v_pk_mul_f32 v[28:29], v[20:21], v[28:29] op_sel:[1,0] op_sel_hi:[0,1]
	v_pk_fma_f32 v[26:27], v[20:21], v[26:27], v[28:29] op_sel_hi:[1,0,1]
	v_xor_b32_e32 v29, 0x80000000, v24
	v_mov_b32_e32 v28, v25
	v_pk_mul_f32 v[28:29], v[28:29], v[26:27] op_sel:[0,1]
	s_nop 0
	v_pk_fma_f32 v[24:25], v[24:25], v[26:27], v[28:29] op_sel_hi:[1,0,1]
	v_xor_b32_e32 v28, 0x80000000, v27
	v_mov_b32_e32 v29, v27
	v_pk_mul_f32 v[28:29], v[20:21], v[28:29] op_sel:[1,0] op_sel_hi:[0,1]
	v_pk_fma_f32 v[26:27], v[20:21], v[26:27], v[28:29] op_sel_hi:[1,0,1]
	v_xad_u32 v28, v50, 2, v10
	v_lshl_add_u32 v51, v28, 3, 0
	ds_read2_b64 v[28:31], v51 offset0:64 offset1:80
	v_xor_b32_e32 v32, 0x80000000, v27
	v_mov_b32_e32 v33, v27
	v_pk_mul_f32 v[32:33], v[20:21], v[32:33] op_sel:[1,0] op_sel_hi:[0,1]
	s_waitcnt lgkmcnt(0)
	v_xor_b32_e32 v35, 0x80000000, v28
	v_mov_b32_e32 v34, v29
	v_pk_mul_f32 v[34:35], v[34:35], v[26:27] op_sel:[0,1]
	s_nop 0
	v_pk_fma_f32 v[28:29], v[28:29], v[26:27], v[34:35] op_sel_hi:[1,0,1]
	v_pk_fma_f32 v[34:35], v[20:21], v[26:27], v[32:33] op_sel_hi:[1,0,1]
	v_xor_b32_e32 v27, 0x80000000, v30
	v_mov_b32_e32 v26, v31
	v_pk_mul_f32 v[26:27], v[26:27], v[34:35] op_sel:[0,1]
	v_xor_b32_e32 v36, 0x80000000, v35
	v_pk_fma_f32 v[26:27], v[30:31], v[34:35], v[26:27] op_sel_hi:[1,0,1]
	v_xad_u32 v30, v50, 3, v10
	v_lshl_add_u32 v54, v30, 3, 0
	ds_read2_b64 v[30:33], v54 offset0:96 offset1:112
	v_mov_b32_e32 v37, v35
	v_pk_mul_f32 v[36:37], v[20:21], v[36:37] op_sel:[1,0] op_sel_hi:[0,1]
	v_pk_fma_f32 v[34:35], v[20:21], v[34:35], v[36:37] op_sel_hi:[1,0,1]
	s_waitcnt lgkmcnt(0)
	v_xor_b32_e32 v37, 0x80000000, v30
	v_mov_b32_e32 v36, v31
	v_pk_mul_f32 v[36:37], v[36:37], v[34:35] op_sel:[0,1]
	s_nop 0
	v_pk_fma_f32 v[30:31], v[30:31], v[34:35], v[36:37] op_sel_hi:[1,0,1]
	v_xor_b32_e32 v36, 0x80000000, v35
	v_mov_b32_e32 v37, v35
	v_pk_mul_f32 v[36:37], v[20:21], v[36:37] op_sel:[1,0] op_sel_hi:[0,1]
	v_pk_fma_f32 v[34:35], v[20:21], v[34:35], v[36:37] op_sel_hi:[1,0,1]
	v_xor_b32_e32 v37, 0x80000000, v32
	v_mov_b32_e32 v36, v33
	v_pk_mul_f32 v[36:37], v[36:37], v[34:35] op_sel:[0,1]
	s_nop 0
	v_pk_fma_f32 v[32:33], v[32:33], v[34:35], v[36:37] op_sel_hi:[1,0,1]
	v_xor_b32_e32 v36, 0x80000000, v35
	v_mov_b32_e32 v37, v35
	v_pk_mul_f32 v[36:37], v[20:21], v[36:37] op_sel:[1,0] op_sel_hi:[0,1]
	v_pk_fma_f32 v[38:39], v[20:21], v[34:35], v[36:37] op_sel_hi:[1,0,1]
	v_xad_u32 v34, v50, 4, v10
	v_lshl_add_u32 v55, v34, 3, 0
	ds_read2_b64 v[34:37], v55 offset0:128 offset1:144
	v_xor_b32_e32 v40, 0x80000000, v39
	v_mov_b32_e32 v41, v39
	v_pk_mul_f32 v[40:41], v[20:21], v[40:41] op_sel:[1,0] op_sel_hi:[0,1]
	s_waitcnt lgkmcnt(0)
	v_xor_b32_e32 v43, 0x80000000, v34
	v_mov_b32_e32 v42, v35
	v_pk_mul_f32 v[42:43], v[42:43], v[38:39] op_sel:[0,1]
	s_nop 0
	v_pk_fma_f32 v[34:35], v[34:35], v[38:39], v[42:43] op_sel_hi:[1,0,1]
	v_pk_fma_f32 v[42:43], v[20:21], v[38:39], v[40:41] op_sel_hi:[1,0,1]
	v_xor_b32_e32 v39, 0x80000000, v36
	v_mov_b32_e32 v38, v37
	v_pk_mul_f32 v[38:39], v[38:39], v[42:43] op_sel:[0,1]
	v_xor_b32_e32 v44, 0x80000000, v43
	v_pk_fma_f32 v[36:37], v[36:37], v[42:43], v[38:39] op_sel_hi:[1,0,1]
	v_xad_u32 v38, v50, 5, v10
	v_lshl_add_u32 v56, v38, 3, 0
	ds_read2_b64 v[38:41], v56 offset0:160 offset1:176
	v_mov_b32_e32 v45, v43
	v_pk_mul_f32 v[44:45], v[20:21], v[44:45] op_sel:[1,0] op_sel_hi:[0,1]
	v_pk_fma_f32 v[42:43], v[20:21], v[42:43], v[44:45] op_sel_hi:[1,0,1]
	s_waitcnt lgkmcnt(0)
	v_xor_b32_e32 v45, 0x80000000, v38
	v_mov_b32_e32 v44, v39
	v_pk_mul_f32 v[44:45], v[44:45], v[42:43] op_sel:[0,1]
	s_nop 0
	v_pk_fma_f32 v[38:39], v[38:39], v[42:43], v[44:45] op_sel_hi:[1,0,1]
	v_xor_b32_e32 v44, 0x80000000, v43
	v_mov_b32_e32 v45, v43
	v_pk_mul_f32 v[44:45], v[20:21], v[44:45] op_sel:[1,0] op_sel_hi:[0,1]
	v_pk_fma_f32 v[42:43], v[20:21], v[42:43], v[44:45] op_sel_hi:[1,0,1]
	v_xor_b32_e32 v45, 0x80000000, v40
	v_mov_b32_e32 v44, v41
	v_pk_mul_f32 v[44:45], v[44:45], v[42:43] op_sel:[0,1]
	s_nop 0
	v_pk_fma_f32 v[40:41], v[40:41], v[42:43], v[44:45] op_sel_hi:[1,0,1]
	v_xor_b32_e32 v44, 0x80000000, v43
	v_mov_b32_e32 v45, v43
	v_pk_mul_f32 v[44:45], v[20:21], v[44:45] op_sel:[1,0] op_sel_hi:[0,1]
	v_pk_fma_f32 v[42:43], v[20:21], v[42:43], v[44:45] op_sel_hi:[1,0,1]
	v_xad_u32 v44, v50, 6, v10
	v_lshl_add_u32 v57, v44, 3, 0
	ds_read2_b64 v[44:47], v57 offset0:192 offset1:208
	v_xor_b32_e32 v48, 0x80000000, v43
	v_mov_b32_e32 v49, v43
	v_pk_mul_f32 v[48:49], v[20:21], v[48:49] op_sel:[1,0] op_sel_hi:[0,1]
	s_waitcnt lgkmcnt(0)
	v_xor_b32_e32 v53, 0x80000000, v44
	v_mov_b32_e32 v52, v45
	v_pk_mul_f32 v[52:53], v[52:53], v[42:43] op_sel:[0,1]
	s_nop 0
	v_pk_fma_f32 v[44:45], v[44:45], v[42:43], v[52:53] op_sel_hi:[1,0,1]
	v_pk_fma_f32 v[52:53], v[20:21], v[42:43], v[48:49] op_sel_hi:[1,0,1]
	v_xor_b32_e32 v43, 0x80000000, v46
	v_mov_b32_e32 v42, v47
	v_pk_mul_f32 v[42:43], v[42:43], v[52:53] op_sel:[0,1]
	v_xor_b32_e32 v60, 0x80000000, v53
	v_pk_fma_f32 v[42:43], v[46:47], v[52:53], v[42:43] op_sel_hi:[1,0,1]
	v_xad_u32 v46, v50, 7, v10
	v_lshl_add_u32 v58, v46, 3, 0
	ds_read2_b64 v[46:49], v58 offset0:224 offset1:240
	v_mov_b32_e32 v61, v53
	v_pk_mul_f32 v[60:61], v[20:21], v[60:61] op_sel:[1,0] op_sel_hi:[0,1]
	v_pk_fma_f32 v[52:53], v[20:21], v[52:53], v[60:61] op_sel_hi:[1,0,1]
	s_waitcnt lgkmcnt(0)
	v_xor_b32_e32 v61, 0x80000000, v46
	v_mov_b32_e32 v60, v47
	v_pk_mul_f32 v[60:61], v[60:61], v[52:53] op_sel:[0,1]
	s_nop 0
	v_pk_fma_f32 v[46:47], v[46:47], v[52:53], v[60:61] op_sel_hi:[1,0,1]
	v_xor_b32_e32 v60, 0x80000000, v53
	v_mov_b32_e32 v61, v53
	v_pk_mul_f32 v[60:61], v[20:21], v[60:61] op_sel:[1,0] op_sel_hi:[0,1]
	v_pk_fma_f32 v[52:53], v[20:21], v[52:53], v[60:61] op_sel_hi:[1,0,1]
	v_xor_b32_e32 v61, 0x80000000, v48
	v_mov_b32_e32 v60, v49
	v_pk_mul_f32 v[60:61], v[60:61], v[52:53] op_sel:[0,1]
	s_nop 0
	v_pk_fma_f32 v[48:49], v[48:49], v[52:53], v[60:61] op_sel_hi:[1,0,1]
	v_xor_b32_e32 v60, 0x80000000, v53
	v_mov_b32_e32 v61, v53
	v_pk_mul_f32 v[60:61], v[20:21], v[60:61] op_sel:[1,0] op_sel_hi:[0,1]
	v_pk_fma_f32 v[64:65], v[20:21], v[52:53], v[60:61] op_sel_hi:[1,0,1]
	v_xad_u32 v52, v50, 8, v10
	v_lshl_add_u32 v52, v52, 3, 0
	v_add_u32_e32 v59, 0x800, v52
	ds_read2_b64 v[60:63], v59 offset1:16
	v_xor_b32_e32 v52, 0x80000000, v65
	v_mov_b32_e32 v53, v65
	v_pk_mul_f32 v[66:67], v[20:21], v[52:53] op_sel:[1,0] op_sel_hi:[0,1]
	v_pk_fma_f32 v[66:67], v[20:21], v[64:65], v[66:67] op_sel_hi:[1,0,1]
	s_waitcnt lgkmcnt(0)
	v_xor_b32_e32 v53, 0x80000000, v60
	v_mov_b32_e32 v52, v61
	v_pk_mul_f32 v[52:53], v[52:53], v[64:65] op_sel:[0,1]
	v_xor_b32_e32 v68, 0x80000000, v67
	v_pk_fma_f32 v[52:53], v[60:61], v[64:65], v[52:53] op_sel_hi:[1,0,1]
	v_xor_b32_e32 v61, 0x80000000, v62
	v_mov_b32_e32 v60, v63
	v_pk_mul_f32 v[60:61], v[60:61], v[66:67] op_sel:[0,1]
	v_mov_b32_e32 v69, v67
	v_pk_fma_f32 v[70:71], v[62:63], v[66:67], v[60:61] op_sel_hi:[1,0,1]
	v_xad_u32 v60, v50, 9, v10
	v_lshl_add_u32 v60, v60, 3, 0
	v_add_u32_e32 v60, 0x800, v60
	ds_read2_b64 v[62:65], v60 offset0:32 offset1:48
	v_pk_mul_f32 v[68:69], v[20:21], v[68:69] op_sel:[1,0] op_sel_hi:[0,1]
	v_pk_fma_f32 v[66:67], v[20:21], v[66:67], v[68:69] op_sel_hi:[1,0,1]
	s_waitcnt lgkmcnt(0)
	v_xor_b32_e32 v69, 0x80000000, v62
	v_mov_b32_e32 v68, v63
	v_pk_mul_f32 v[68:69], v[68:69], v[66:67] op_sel:[0,1]
	s_nop 0
	v_pk_fma_f32 v[72:73], v[62:63], v[66:67], v[68:69] op_sel_hi:[1,0,1]
	v_xor_b32_e32 v62, 0x80000000, v67
	v_mov_b32_e32 v63, v67
	v_pk_mul_f32 v[62:63], v[20:21], v[62:63] op_sel:[1,0] op_sel_hi:[0,1]
	v_pk_fma_f32 v[62:63], v[20:21], v[66:67], v[62:63] op_sel_hi:[1,0,1]
	v_xor_b32_e32 v67, 0x80000000, v64
	v_mov_b32_e32 v66, v65
	v_pk_mul_f32 v[66:67], v[66:67], v[62:63] op_sel:[0,1]
	s_nop 0
	v_pk_fma_f32 v[74:75], v[64:65], v[62:63], v[66:67] op_sel_hi:[1,0,1]
	v_xor_b32_e32 v64, 0x80000000, v63
	v_mov_b32_e32 v65, v63
	v_pk_mul_f32 v[64:65], v[20:21], v[64:65] op_sel:[1,0] op_sel_hi:[0,1]
	v_pk_fma_f32 v[66:67], v[20:21], v[62:63], v[64:65] op_sel_hi:[1,0,1]
	v_xad_u32 v61, v50, 10, v10
	v_lshl_add_u32 v61, v61, 3, 0
	v_add_u32_e32 v61, 0x800, v61
	ds_read2_b64 v[62:65], v61 offset0:64 offset1:80
	v_xor_b32_e32 v68, 0x80000000, v67
	v_mov_b32_e32 v69, v67
	v_pk_mul_f32 v[68:69], v[20:21], v[68:69] op_sel:[1,0] op_sel_hi:[0,1]
	v_pk_fma_f32 v[68:69], v[20:21], v[66:67], v[68:69] op_sel_hi:[1,0,1]
	s_waitcnt lgkmcnt(0)
	v_xor_b32_e32 v77, 0x80000000, v62
	v_mov_b32_e32 v76, v63
	v_pk_mul_f32 v[76:77], v[76:77], v[66:67] op_sel:[0,1]
	v_xor_b32_e32 v80, 0x80000000, v69
	v_pk_fma_f32 v[76:77], v[62:63], v[66:67], v[76:77] op_sel_hi:[1,0,1]
	v_xor_b32_e32 v63, 0x80000000, v64
	v_mov_b32_e32 v62, v65
	v_pk_mul_f32 v[62:63], v[62:63], v[68:69] op_sel:[0,1]
	v_mov_b32_e32 v81, v69
	v_pk_fma_f32 v[78:79], v[64:65], v[68:69], v[62:63] op_sel_hi:[1,0,1]
	v_xad_u32 v62, v50, 11, v10
	v_lshl_add_u32 v62, v62, 3, 0
	v_add_u32_e32 v62, 0x800, v62
	ds_read2_b64 v[64:67], v62 offset0:96 offset1:112
	v_pk_mul_f32 v[80:81], v[20:21], v[80:81] op_sel:[1,0] op_sel_hi:[0,1]
	v_pk_fma_f32 v[68:69], v[20:21], v[68:69], v[80:81] op_sel_hi:[1,0,1]
	s_waitcnt lgkmcnt(0)
	v_xor_b32_e32 v81, 0x80000000, v64
	v_mov_b32_e32 v80, v65
	v_pk_mul_f32 v[80:81], v[80:81], v[68:69] op_sel:[0,1]
	s_nop 0
	v_pk_fma_f32 v[80:81], v[64:65], v[68:69], v[80:81] op_sel_hi:[1,0,1]
	v_xor_b32_e32 v64, 0x80000000, v69
	v_mov_b32_e32 v65, v69
	v_pk_mul_f32 v[64:65], v[20:21], v[64:65] op_sel:[1,0] op_sel_hi:[0,1]
	v_pk_fma_f32 v[64:65], v[20:21], v[68:69], v[64:65] op_sel_hi:[1,0,1]
	v_xor_b32_e32 v69, 0x80000000, v66
	v_mov_b32_e32 v68, v67
	v_pk_mul_f32 v[68:69], v[68:69], v[64:65] op_sel:[0,1]
	s_nop 0
	v_pk_fma_f32 v[82:83], v[66:67], v[64:65], v[68:69] op_sel_hi:[1,0,1]
	v_xor_b32_e32 v66, 0x80000000, v65
	v_mov_b32_e32 v67, v65
	v_pk_mul_f32 v[66:67], v[20:21], v[66:67] op_sel:[1,0] op_sel_hi:[0,1]
	v_pk_fma_f32 v[68:69], v[20:21], v[64:65], v[66:67] op_sel_hi:[1,0,1]
	v_xad_u32 v63, v50, 12, v10
	v_lshl_add_u32 v63, v63, 3, 0
	v_add_u32_e32 v63, 0x800, v63
	ds_read2_b64 v[64:67], v63 offset0:128 offset1:144
	v_xor_b32_e32 v84, 0x80000000, v69
	v_mov_b32_e32 v85, v69
	v_pk_mul_f32 v[84:85], v[20:21], v[84:85] op_sel:[1,0] op_sel_hi:[0,1]
	v_pk_fma_f32 v[84:85], v[20:21], v[68:69], v[84:85] op_sel_hi:[1,0,1]
	s_waitcnt lgkmcnt(0)
	v_xor_b32_e32 v87, 0x80000000, v64
	v_mov_b32_e32 v86, v65
	v_pk_mul_f32 v[86:87], v[86:87], v[68:69] op_sel:[0,1]
	v_xor_b32_e32 v90, 0x80000000, v85
	v_pk_fma_f32 v[86:87], v[64:65], v[68:69], v[86:87] op_sel_hi:[1,0,1]
	v_xor_b32_e32 v65, 0x80000000, v66
	v_mov_b32_e32 v64, v67
	v_pk_mul_f32 v[64:65], v[64:65], v[84:85] op_sel:[0,1]
	v_mov_b32_e32 v91, v85
	v_pk_fma_f32 v[88:89], v[66:67], v[84:85], v[64:65] op_sel_hi:[1,0,1]
	v_xad_u32 v64, v50, 13, v10
	v_lshl_add_u32 v64, v64, 3, 0
	v_add_u32_e32 v64, 0x800, v64
	ds_read2_b64 v[66:69], v64 offset0:160 offset1:176
	v_pk_mul_f32 v[90:91], v[20:21], v[90:91] op_sel:[1,0] op_sel_hi:[0,1]
	v_pk_fma_f32 v[84:85], v[20:21], v[84:85], v[90:91] op_sel_hi:[1,0,1]
	s_waitcnt lgkmcnt(0)
	v_xor_b32_e32 v91, 0x80000000, v66
	v_mov_b32_e32 v90, v67
	v_pk_mul_f32 v[90:91], v[90:91], v[84:85] op_sel:[0,1]
	s_nop 0
	v_pk_fma_f32 v[90:91], v[66:67], v[84:85], v[90:91] op_sel_hi:[1,0,1]
	v_xor_b32_e32 v66, 0x80000000, v85
	v_mov_b32_e32 v67, v85
	v_pk_mul_f32 v[66:67], v[20:21], v[66:67] op_sel:[1,0] op_sel_hi:[0,1]
	v_pk_fma_f32 v[66:67], v[20:21], v[84:85], v[66:67] op_sel_hi:[1,0,1]
	v_xor_b32_e32 v85, 0x80000000, v68
	v_mov_b32_e32 v84, v69
	v_pk_mul_f32 v[84:85], v[84:85], v[66:67] op_sel:[0,1]
	s_nop 0
	v_pk_fma_f32 v[84:85], v[68:69], v[66:67], v[84:85] op_sel_hi:[1,0,1]
	v_xor_b32_e32 v68, 0x80000000, v67
	v_mov_b32_e32 v69, v67
	v_pk_mul_f32 v[68:69], v[20:21], v[68:69] op_sel:[1,0] op_sel_hi:[0,1]
	v_pk_fma_f32 v[92:93], v[20:21], v[66:67], v[68:69] op_sel_hi:[1,0,1]
	v_xad_u32 v65, v50, 14, v10
	v_lshl_add_u32 v65, v65, 3, 0
	v_add_u32_e32 v65, 0x800, v65
	ds_read2_b64 v[66:69], v65 offset0:192 offset1:208
	v_xor_b32_e32 v94, 0x80000000, v93
	v_mov_b32_e32 v95, v93
	v_pk_mul_f32 v[94:95], v[20:21], v[94:95] op_sel:[1,0] op_sel_hi:[0,1]
	v_xad_u32 v10, v50, 15, v10
	s_waitcnt lgkmcnt(0)
	v_xor_b32_e32 v97, 0x80000000, v66
	v_mov_b32_e32 v96, v67
	v_pk_mul_f32 v[96:97], v[96:97], v[92:93] op_sel:[0,1]
	v_lshl_add_u32 v10, v10, 3, 0
	v_pk_fma_f32 v[96:97], v[66:67], v[92:93], v[96:97] op_sel_hi:[1,0,1]
	v_pk_fma_f32 v[92:93], v[20:21], v[92:93], v[94:95] op_sel_hi:[1,0,1]
	v_xor_b32_e32 v67, 0x80000000, v68
	v_mov_b32_e32 v66, v69
	v_pk_mul_f32 v[66:67], v[66:67], v[92:93] op_sel:[0,1]
	v_add_u32_e32 v101, 0x800, v10
	v_pk_fma_f32 v[94:95], v[68:69], v[92:93], v[66:67] op_sel_hi:[1,0,1]
	ds_read2_b64 v[66:69], v101 offset0:224 offset1:240
	v_xor_b32_e32 v98, 0x80000000, v93
	v_mov_b32_e32 v99, v93
	v_pk_mul_f32 v[98:99], v[20:21], v[98:99] op_sel:[1,0] op_sel_hi:[0,1]
	v_pk_fma_f32 v[92:93], v[20:21], v[92:93], v[98:99] op_sel_hi:[1,0,1]
	s_waitcnt lgkmcnt(0)
	v_xor_b32_e32 v99, 0x80000000, v66
	v_mov_b32_e32 v98, v67
	v_pk_mul_f32 v[98:99], v[98:99], v[92:93] op_sel:[0,1]
	s_nop 0
	v_pk_fma_f32 v[66:67], v[66:67], v[92:93], v[98:99] op_sel_hi:[1,0,1]
	v_xor_b32_e32 v98, 0x80000000, v93
	v_mov_b32_e32 v99, v93
	v_pk_mul_f32 v[98:99], v[20:21], v[98:99] op_sel:[1,0] op_sel_hi:[0,1]
	v_pk_fma_f32 v[20:21], v[20:21], v[92:93], v[98:99] op_sel_hi:[1,0,1]
	v_xor_b32_e32 v93, 0x80000000, v68
	v_mov_b32_e32 v92, v69
	v_pk_mul_f32 v[92:93], v[92:93], v[20:21] op_sel:[0,1]
	s_nop 0
	v_pk_fma_f32 v[68:69], v[68:69], v[20:21], v[92:93] op_sel_hi:[1,0,1]
	v_mov_b32_e32 v10, v1
	v_pk_add_f32 v[104:105], v[16:17], v[52:53]
	v_pk_add_f32 v[16:17], v[16:17], v[52:53] neg_lo:[0,1] neg_hi:[0,1]
	v_pk_add_f32 v[52:53], v[18:19], v[70:71]
	v_pk_add_f32 v[18:19], v[18:19], v[70:71] neg_lo:[0,1] neg_hi:[0,1]
	v_mov_b32_e32 v92, v164
	v_mov_b32_e32 v20, v165
	v_mov_b32_e32 v98, v166
	v_mov_b32_e32 v10, v167
	v_mov_b32_e32 v100, v168
	v_mov_b32_e32 v50, v169
	v_mov_b32_e32 v102, v170
	v_xor_b32_e32 v70, 0x80000000, v19
	v_mov_b32_e32 v71, v18
	v_mov_b32_e32 v21, v171
	v_pk_mul_f32 v[70:71], v[102:103], v[70:71] op_sel_hi:[0,1]
	v_pk_fma_f32 v[18:19], v[92:93], v[18:19], v[70:71] op_sel_hi:[0,1,1]
	v_pk_add_f32 v[70:71], v[22:23], v[72:73]
	v_pk_add_f32 v[22:23], v[22:23], v[72:73] neg_lo:[0,1] neg_hi:[0,1]
	s_nop 0
	v_xor_b32_e32 v72, 0x80000000, v23
	v_mov_b32_e32 v73, v22
	v_pk_mul_f32 v[72:73], v[50:51], v[72:73] op_sel_hi:[0,1]
	v_pk_fma_f32 v[22:23], v[20:21], v[22:23], v[72:73] op_sel_hi:[0,1,1]
	v_pk_add_f32 v[72:73], v[24:25], v[74:75]
	v_pk_add_f32 v[24:25], v[24:25], v[74:75] neg_lo:[0,1] neg_hi:[0,1]
	s_nop 0
	v_xor_b32_e32 v74, 0x80000000, v25
	v_mov_b32_e32 v75, v24
	v_pk_mul_f32 v[74:75], v[100:101], v[74:75] op_sel_hi:[0,1]
	v_pk_fma_f32 v[24:25], v[98:99], v[24:25], v[74:75] op_sel_hi:[0,1,1]
	v_pk_add_f32 v[74:75], v[28:29], v[76:77]
	v_pk_add_f32 v[28:29], v[28:29], v[76:77] neg_lo:[0,1] neg_hi:[0,1]
	s_nop 0
	v_xor_b32_e32 v76, 0x80000000, v29
	v_mov_b32_e32 v77, v28
	v_pk_mul_f32 v[76:77], v[10:11], v[76:77] op_sel_hi:[0,1]
	v_pk_fma_f32 v[28:29], v[10:11], v[28:29], v[76:77] op_sel_hi:[0,1,1]
	v_pk_add_f32 v[76:77], v[26:27], v[78:79]
	v_pk_add_f32 v[26:27], v[26:27], v[78:79] neg_lo:[0,1] neg_hi:[0,1]
	s_nop 0
	v_xor_b32_e32 v78, 0x80000000, v27
	v_mov_b32_e32 v79, v26
	v_pk_mul_f32 v[78:79], v[98:99], v[78:79] op_sel_hi:[0,1]
	v_pk_fma_f32 v[26:27], v[100:101], v[26:27], v[78:79] op_sel_hi:[0,1,1]
	v_pk_add_f32 v[78:79], v[30:31], v[80:81]
	v_pk_add_f32 v[30:31], v[30:31], v[80:81] neg_lo:[0,1] neg_hi:[0,1]
	s_nop 0
	v_xor_b32_e32 v80, 0x80000000, v31
	v_mov_b32_e32 v81, v30
	v_pk_mul_f32 v[80:81], v[20:21], v[80:81] op_sel_hi:[0,1]
	v_pk_fma_f32 v[30:31], v[50:51], v[30:31], v[80:81] op_sel_hi:[0,1,1]
	v_pk_add_f32 v[80:81], v[32:33], v[82:83]
	v_pk_add_f32 v[32:33], v[32:33], v[82:83] neg_lo:[0,1] neg_hi:[0,1]
	s_nop 0
	v_xor_b32_e32 v82, 0x80000000, v33
	v_mov_b32_e32 v83, v32
	v_pk_mul_f32 v[82:83], v[92:93], v[82:83] op_sel_hi:[0,1]
	v_pk_fma_f32 v[32:33], v[102:103], v[32:33], v[82:83] op_sel_hi:[0,1,1]
	v_pk_add_f32 v[82:83], v[34:35], v[86:87]
	v_pk_add_f32 v[34:35], v[34:35], v[86:87] neg_lo:[0,1] neg_hi:[0,1]
	s_nop 0
	v_xor_b32_e32 v86, 0x80000000, v35
	v_mov_b32_e32 v87, v34
	v_pk_add_f32 v[34:35], v[36:37], v[88:89]
	v_pk_add_f32 v[36:37], v[36:37], v[88:89] neg_lo:[0,1] neg_hi:[0,1]
	s_nop 0
	v_xor_b32_e32 v88, 0x80000000, v37
	v_mov_b32_e32 v89, v36
	v_pk_mul_f32 v[88:89], v[92:93], v[88:89] op_sel_hi:[0,1]
	v_pk_fma_f32 v[36:37], v[102:103], v[36:37], v[88:89] op_sel_hi:[0,1,1] neg_lo:[1,0,0] neg_hi:[1,0,0]
	v_pk_add_f32 v[88:89], v[38:39], v[90:91]
	v_pk_add_f32 v[38:39], v[38:39], v[90:91] neg_lo:[0,1] neg_hi:[0,1]
	s_nop 0
	v_xor_b32_e32 v90, 0x80000000, v39
	v_mov_b32_e32 v91, v38
	v_pk_mul_f32 v[90:91], v[20:21], v[90:91] op_sel_hi:[0,1]
	v_pk_fma_f32 v[38:39], v[50:51], v[38:39], v[90:91] op_sel_hi:[0,1,1] neg_lo:[1,0,0] neg_hi:[1,0,0]
	v_pk_add_f32 v[90:91], v[40:41], v[84:85]
	v_pk_add_f32 v[40:41], v[40:41], v[84:85] neg_lo:[0,1] neg_hi:[0,1]
	s_nop 0
	v_xor_b32_e32 v84, 0x80000000, v41
	v_mov_b32_e32 v85, v40
	v_pk_mul_f32 v[84:85], v[98:99], v[84:85] op_sel_hi:[0,1]
	v_pk_fma_f32 v[40:41], v[100:101], v[40:41], v[84:85] op_sel_hi:[0,1,1] neg_lo:[1,0,0] neg_hi:[1,0,0]
	v_pk_add_f32 v[84:85], v[44:45], v[96:97]
	v_pk_add_f32 v[44:45], v[44:45], v[96:97] neg_lo:[0,1] neg_hi:[0,1]
	s_nop 0
	v_xor_b32_e32 v96, 0x80000000, v45
	v_mov_b32_e32 v97, v44
	v_pk_mul_f32 v[96:97], v[10:11], v[96:97] op_sel_hi:[0,1]
	v_pk_fma_f32 v[44:45], v[10:11], v[44:45], v[96:97] op_sel_hi:[0,1,1] neg_lo:[1,0,0] neg_hi:[1,0,0]
	v_pk_add_f32 v[96:97], v[42:43], v[94:95]
	v_pk_add_f32 v[42:43], v[42:43], v[94:95] neg_lo:[0,1] neg_hi:[0,1]
	s_nop 0
	v_xor_b32_e32 v94, 0x80000000, v43
	v_mov_b32_e32 v95, v42
	v_pk_mul_f32 v[94:95], v[100:101], v[94:95] op_sel_hi:[0,1]
	v_pk_fma_f32 v[42:43], v[98:99], v[42:43], v[94:95] op_sel_hi:[0,1,1] neg_lo:[1,0,0] neg_hi:[1,0,0]
	v_pk_add_f32 v[94:95], v[46:47], v[66:67]
	v_pk_add_f32 v[46:47], v[46:47], v[66:67] neg_lo:[0,1] neg_hi:[0,1]
	s_nop 0
	v_xor_b32_e32 v66, 0x80000000, v47
	v_mov_b32_e32 v67, v46
	v_pk_mul_f32 v[66:67], v[50:51], v[66:67] op_sel_hi:[0,1]
	v_pk_fma_f32 v[46:47], v[20:21], v[46:47], v[66:67] op_sel_hi:[0,1,1] neg_lo:[1,0,0] neg_hi:[1,0,0]
	v_pk_add_f32 v[66:67], v[48:49], v[68:69]
	v_pk_add_f32 v[48:49], v[48:49], v[68:69] neg_lo:[0,1] neg_hi:[0,1]
	s_nop 0
	v_xor_b32_e32 v68, 0x80000000, v49
	v_mov_b32_e32 v69, v48
	v_pk_mul_f32 v[68:69], v[102:103], v[68:69] op_sel_hi:[0,1]
	v_pk_fma_f32 v[48:49], v[92:93], v[48:49], v[68:69] op_sel_hi:[0,1,1] neg_lo:[1,0,0] neg_hi:[1,0,0]
	v_pk_add_f32 v[92:93], v[52:53], v[34:35]
	v_pk_add_f32 v[34:35], v[52:53], v[34:35] neg_lo:[0,1] neg_hi:[0,1]
	v_pk_add_f32 v[68:69], v[104:105], v[82:83]
	v_xor_b32_e32 v52, 0x80000000, v35
	v_mov_b32_e32 v53, v34
	v_pk_mul_f32 v[52:53], v[50:51], v[52:53] op_sel_hi:[0,1]
	v_pk_fma_f32 v[34:35], v[20:21], v[34:35], v[52:53] op_sel_hi:[0,1,1]
	v_pk_add_f32 v[52:53], v[70:71], v[88:89]
	v_pk_add_f32 v[70:71], v[70:71], v[88:89] neg_lo:[0,1] neg_hi:[0,1]
	v_pk_add_f32 v[82:83], v[104:105], v[82:83] neg_lo:[0,1] neg_hi:[0,1]
	v_xor_b32_e32 v88, 0x80000000, v71
	v_mov_b32_e32 v89, v70
	v_pk_mul_f32 v[88:89], v[10:11], v[88:89] op_sel_hi:[0,1]
	v_pk_fma_f32 v[70:71], v[10:11], v[70:71], v[88:89] op_sel_hi:[0,1,1]
	v_pk_add_f32 v[88:89], v[72:73], v[90:91]
	v_pk_add_f32 v[72:73], v[72:73], v[90:91] neg_lo:[0,1] neg_hi:[0,1]
	s_nop 0
	v_xor_b32_e32 v90, 0x80000000, v73
	v_mov_b32_e32 v91, v72
	v_pk_mul_f32 v[90:91], v[20:21], v[90:91] op_sel_hi:[0,1]
	v_pk_fma_f32 v[72:73], v[50:51], v[72:73], v[90:91] op_sel_hi:[0,1,1]
	v_pk_add_f32 v[90:91], v[74:75], v[84:85]
	v_pk_add_f32 v[74:75], v[74:75], v[84:85] neg_lo:[0,1] neg_hi:[0,1]
	s_nop 0
	v_xor_b32_e32 v84, 0x80000000, v75
	v_mov_b32_e32 v85, v74
	v_pk_add_f32 v[74:75], v[76:77], v[96:97]
	v_pk_add_f32 v[76:77], v[76:77], v[96:97] neg_lo:[0,1] neg_hi:[0,1]
	s_nop 0
	v_xor_b32_e32 v96, 0x80000000, v77
	v_mov_b32_e32 v97, v76
	v_pk_mul_f32 v[96:97], v[20:21], v[96:97] op_sel_hi:[0,1]
	v_pk_fma_f32 v[76:77], v[50:51], v[76:77], v[96:97] op_sel_hi:[0,1,1] neg_lo:[1,0,0] neg_hi:[1,0,0]
	v_pk_add_f32 v[96:97], v[78:79], v[94:95]
	v_pk_add_f32 v[78:79], v[78:79], v[94:95] neg_lo:[0,1] neg_hi:[0,1]
	s_nop 0
	v_xor_b32_e32 v94, 0x80000000, v79
	v_mov_b32_e32 v95, v78
	v_pk_mul_f32 v[94:95], v[10:11], v[94:95] op_sel_hi:[0,1]
	v_pk_fma_f32 v[78:79], v[10:11], v[78:79], v[94:95] op_sel_hi:[0,1,1] neg_lo:[1,0,0] neg_hi:[1,0,0]
	v_pk_add_f32 v[94:95], v[80:81], v[66:67]
	v_pk_add_f32 v[66:67], v[80:81], v[66:67] neg_lo:[0,1] neg_hi:[0,1]
	s_nop 0
	v_xor_b32_e32 v80, 0x80000000, v67
	v_mov_b32_e32 v81, v66
	v_pk_mul_f32 v[80:81], v[50:51], v[80:81] op_sel_hi:[0,1]
	v_pk_fma_f32 v[66:67], v[20:21], v[66:67], v[80:81] op_sel_hi:[0,1,1] neg_lo:[1,0,0] neg_hi:[1,0,0]
	v_pk_add_f32 v[80:81], v[68:69], v[90:91]
	v_pk_add_f32 v[68:69], v[68:69], v[90:91] neg_lo:[0,1] neg_hi:[0,1]
	v_pk_add_f32 v[90:91], v[92:93], v[74:75]
	v_pk_add_f32 v[74:75], v[92:93], v[74:75] neg_lo:[0,1] neg_hi:[0,1]
	s_nop 0
	v_xor_b32_e32 v92, 0x80000000, v75
	v_mov_b32_e32 v93, v74
	v_pk_mul_f32 v[92:93], v[10:11], v[92:93] op_sel_hi:[0,1]
	v_pk_fma_f32 v[74:75], v[10:11], v[74:75], v[92:93] op_sel_hi:[0,1,1]
	v_pk_add_f32 v[92:93], v[52:53], v[96:97]
	v_pk_add_f32 v[52:53], v[52:53], v[96:97] neg_lo:[0,1] neg_hi:[0,1]
	s_nop 0
	v_xor_b32_e32 v96, 0x80000000, v53
	v_mov_b32_e32 v97, v52
	v_pk_add_f32 v[52:53], v[88:89], v[94:95]
	v_pk_add_f32 v[88:89], v[88:89], v[94:95] neg_lo:[0,1] neg_hi:[0,1]
	s_nop 0
	v_xor_b32_e32 v94, 0x80000000, v89
	v_mov_b32_e32 v95, v88
	v_pk_mul_f32 v[94:95], v[10:11], v[94:95] op_sel_hi:[0,1]
	v_pk_fma_f32 v[88:89], v[10:11], v[88:89], v[94:95] op_sel_hi:[0,1,1] neg_lo:[1,0,0] neg_hi:[1,0,0]
	v_pk_add_f32 v[94:95], v[80:81], v[92:93]
	v_pk_add_f32 v[80:81], v[80:81], v[92:93] neg_lo:[0,1] neg_hi:[0,1]
	v_pk_add_f32 v[92:93], v[90:91], v[52:53]
	v_pk_add_f32 v[52:53], v[90:91], v[52:53] neg_lo:[0,1] neg_hi:[0,1]
	s_nop 0
	v_xor_b32_e32 v90, 0x80000000, v53
	v_mov_b32_e32 v91, v52
	v_pk_add_f32 v[52:53], v[94:95], v[92:93]
	v_pk_add_f32 v[92:93], v[94:95], v[92:93] neg_lo:[0,1] neg_hi:[0,1]
	v_pk_add_f32 v[94:95], v[80:81], v[90:91]
	v_pk_add_f32 v[80:81], v[80:81], v[90:91] neg_lo:[0,1] neg_hi:[0,1]
	v_pk_add_f32 v[90:91], v[68:69], v[96:97]
	v_pk_add_f32 v[68:69], v[68:69], v[96:97] neg_lo:[0,1] neg_hi:[0,1]
	v_pk_add_f32 v[96:97], v[74:75], v[88:89]
	v_pk_add_f32 v[74:75], v[74:75], v[88:89] neg_lo:[0,1] neg_hi:[0,1]
	s_nop 0
	v_xor_b32_e32 v88, 0x80000000, v75
	v_mov_b32_e32 v89, v74
	v_pk_add_f32 v[74:75], v[90:91], v[96:97]
	v_pk_add_f32 v[90:91], v[90:91], v[96:97] neg_lo:[0,1] neg_hi:[0,1]
	v_pk_add_f32 v[96:97], v[68:69], v[88:89]
	v_pk_add_f32 v[68:69], v[68:69], v[88:89] neg_lo:[0,1] neg_hi:[0,1]
	v_pk_add_f32 v[88:89], v[82:83], v[84:85]
	v_pk_add_f32 v[82:83], v[82:83], v[84:85] neg_lo:[0,1] neg_hi:[0,1]
	v_pk_add_f32 v[84:85], v[34:35], v[76:77]
	v_pk_add_f32 v[34:35], v[34:35], v[76:77] neg_lo:[0,1] neg_hi:[0,1]
	s_nop 0
	v_xor_b32_e32 v76, 0x80000000, v35
	v_mov_b32_e32 v77, v34
	v_pk_mul_f32 v[76:77], v[10:11], v[76:77] op_sel_hi:[0,1]
	v_pk_fma_f32 v[34:35], v[10:11], v[34:35], v[76:77] op_sel_hi:[0,1,1]
	v_pk_add_f32 v[76:77], v[70:71], v[78:79]
	v_pk_add_f32 v[70:71], v[70:71], v[78:79] neg_lo:[0,1] neg_hi:[0,1]
	s_nop 0
	v_xor_b32_e32 v78, 0x80000000, v71
	v_mov_b32_e32 v79, v70
	v_pk_add_f32 v[70:71], v[72:73], v[66:67]
	v_pk_add_f32 v[66:67], v[72:73], v[66:67] neg_lo:[0,1] neg_hi:[0,1]
	s_nop 0
	v_xor_b32_e32 v72, 0x80000000, v67
	v_mov_b32_e32 v73, v66
	v_pk_mul_f32 v[72:73], v[10:11], v[72:73] op_sel_hi:[0,1]
	v_pk_fma_f32 v[66:67], v[10:11], v[66:67], v[72:73] op_sel_hi:[0,1,1] neg_lo:[1,0,0] neg_hi:[1,0,0]
	v_pk_add_f32 v[72:73], v[88:89], v[76:77]
	v_pk_add_f32 v[76:77], v[88:89], v[76:77] neg_lo:[0,1] neg_hi:[0,1]
	v_pk_add_f32 v[88:89], v[84:85], v[70:71]
	v_pk_add_f32 v[70:71], v[84:85], v[70:71] neg_lo:[0,1] neg_hi:[0,1]
	s_nop 0
	v_xor_b32_e32 v84, 0x80000000, v71
	v_mov_b32_e32 v85, v70
	v_pk_add_f32 v[70:71], v[72:73], v[88:89]
	v_pk_add_f32 v[72:73], v[72:73], v[88:89] neg_lo:[0,1] neg_hi:[0,1]
	v_pk_add_f32 v[88:89], v[76:77], v[84:85]
	v_pk_add_f32 v[76:77], v[76:77], v[84:85] neg_lo:[0,1] neg_hi:[0,1]
	v_pk_add_f32 v[84:85], v[82:83], v[78:79]
	v_pk_add_f32 v[78:79], v[82:83], v[78:79] neg_lo:[0,1] neg_hi:[0,1]
	v_pk_add_f32 v[82:83], v[34:35], v[66:67]
	v_pk_add_f32 v[34:35], v[34:35], v[66:67] neg_lo:[0,1] neg_hi:[0,1]
	s_nop 0
	v_xor_b32_e32 v66, 0x80000000, v35
	v_mov_b32_e32 v67, v34
	v_pk_add_f32 v[34:35], v[84:85], v[82:83]
	v_pk_add_f32 v[82:83], v[84:85], v[82:83] neg_lo:[0,1] neg_hi:[0,1]
	v_pk_add_f32 v[84:85], v[78:79], v[66:67]
	v_pk_add_f32 v[66:67], v[78:79], v[66:67] neg_lo:[0,1] neg_hi:[0,1]
	v_pk_add_f32 v[78:79], v[16:17], v[86:87]
	v_pk_add_f32 v[16:17], v[16:17], v[86:87] neg_lo:[0,1] neg_hi:[0,1]
	v_pk_add_f32 v[86:87], v[18:19], v[36:37]
	v_pk_add_f32 v[18:19], v[18:19], v[36:37] neg_lo:[0,1] neg_hi:[0,1]
	s_nop 0
	v_xor_b32_e32 v36, 0x80000000, v19
	v_mov_b32_e32 v37, v18
	v_pk_mul_f32 v[36:37], v[50:51], v[36:37] op_sel_hi:[0,1]
	v_pk_fma_f32 v[18:19], v[20:21], v[18:19], v[36:37] op_sel_hi:[0,1,1]
	v_pk_add_f32 v[36:37], v[22:23], v[38:39]
	v_pk_add_f32 v[22:23], v[22:23], v[38:39] neg_lo:[0,1] neg_hi:[0,1]
	s_nop 0
	v_xor_b32_e32 v38, 0x80000000, v23
	v_mov_b32_e32 v39, v22
	v_pk_mul_f32 v[38:39], v[10:11], v[38:39] op_sel_hi:[0,1]
	v_pk_fma_f32 v[22:23], v[10:11], v[22:23], v[38:39] op_sel_hi:[0,1,1]
	v_pk_add_f32 v[38:39], v[24:25], v[40:41]
	v_pk_add_f32 v[24:25], v[24:25], v[40:41] neg_lo:[0,1] neg_hi:[0,1]
	s_nop 0
	v_xor_b32_e32 v40, 0x80000000, v25
	v_mov_b32_e32 v41, v24
	v_pk_mul_f32 v[40:41], v[20:21], v[40:41] op_sel_hi:[0,1]
	v_pk_fma_f32 v[24:25], v[50:51], v[24:25], v[40:41] op_sel_hi:[0,1,1]
	v_pk_add_f32 v[40:41], v[28:29], v[44:45]
	v_pk_add_f32 v[28:29], v[28:29], v[44:45] neg_lo:[0,1] neg_hi:[0,1]
	s_nop 0
	v_xor_b32_e32 v44, 0x80000000, v29
	v_mov_b32_e32 v45, v28
	v_pk_add_f32 v[28:29], v[26:27], v[42:43]
	v_pk_add_f32 v[26:27], v[26:27], v[42:43] neg_lo:[0,1] neg_hi:[0,1]
	s_nop 0
	v_xor_b32_e32 v42, 0x80000000, v27
	v_mov_b32_e32 v43, v26
	v_pk_mul_f32 v[42:43], v[20:21], v[42:43] op_sel_hi:[0,1]
	v_pk_fma_f32 v[26:27], v[50:51], v[26:27], v[42:43] op_sel_hi:[0,1,1] neg_lo:[1,0,0] neg_hi:[1,0,0]
	v_pk_add_f32 v[42:43], v[30:31], v[46:47]
	v_pk_add_f32 v[30:31], v[30:31], v[46:47] neg_lo:[0,1] neg_hi:[0,1]
	s_nop 0
	v_xor_b32_e32 v46, 0x80000000, v31
	v_mov_b32_e32 v47, v30
	v_pk_mul_f32 v[46:47], v[10:11], v[46:47] op_sel_hi:[0,1]
	v_pk_fma_f32 v[30:31], v[10:11], v[30:31], v[46:47] op_sel_hi:[0,1,1] neg_lo:[1,0,0] neg_hi:[1,0,0]
	v_pk_add_f32 v[46:47], v[32:33], v[48:49]
	v_pk_add_f32 v[32:33], v[32:33], v[48:49] neg_lo:[0,1] neg_hi:[0,1]
	s_nop 0
	v_xor_b32_e32 v48, 0x80000000, v33
	v_mov_b32_e32 v49, v32
	v_pk_mul_f32 v[48:49], v[50:51], v[48:49] op_sel_hi:[0,1]
	v_pk_fma_f32 v[20:21], v[20:21], v[32:33], v[48:49] op_sel_hi:[0,1,1] neg_lo:[1,0,0] neg_hi:[1,0,0]
	v_pk_add_f32 v[48:49], v[86:87], v[28:29]
	v_pk_add_f32 v[28:29], v[86:87], v[28:29] neg_lo:[0,1] neg_hi:[0,1]
	v_pk_add_f32 v[32:33], v[78:79], v[40:41]
	v_pk_add_f32 v[40:41], v[78:79], v[40:41] neg_lo:[0,1] neg_hi:[0,1]
	v_xor_b32_e32 v78, 0x80000000, v29
	v_mov_b32_e32 v79, v28
	v_pk_mul_f32 v[78:79], v[10:11], v[78:79] op_sel_hi:[0,1]
	v_pk_fma_f32 v[28:29], v[10:11], v[28:29], v[78:79] op_sel_hi:[0,1,1]
	v_pk_add_f32 v[78:79], v[36:37], v[42:43]
	v_pk_add_f32 v[36:37], v[36:37], v[42:43] neg_lo:[0,1] neg_hi:[0,1]
	s_nop 0
	v_xor_b32_e32 v42, 0x80000000, v37
	v_mov_b32_e32 v43, v36
	v_pk_add_f32 v[36:37], v[38:39], v[46:47]
	v_pk_add_f32 v[38:39], v[38:39], v[46:47] neg_lo:[0,1] neg_hi:[0,1]
	s_nop 0
	v_xor_b32_e32 v46, 0x80000000, v39
	v_mov_b32_e32 v47, v38
	v_pk_mul_f32 v[46:47], v[10:11], v[46:47] op_sel_hi:[0,1]
	v_pk_fma_f32 v[38:39], v[10:11], v[38:39], v[46:47] op_sel_hi:[0,1,1] neg_lo:[1,0,0] neg_hi:[1,0,0]
	v_pk_add_f32 v[46:47], v[32:33], v[78:79]
	v_pk_add_f32 v[32:33], v[32:33], v[78:79] neg_lo:[0,1] neg_hi:[0,1]
	v_pk_add_f32 v[78:79], v[48:49], v[36:37]
	v_pk_add_f32 v[36:37], v[48:49], v[36:37] neg_lo:[0,1] neg_hi:[0,1]
	s_nop 0
	v_xor_b32_e32 v48, 0x80000000, v37
	v_mov_b32_e32 v49, v36
	v_pk_add_f32 v[86:87], v[32:33], v[48:49]
	v_pk_add_f32 v[32:33], v[32:33], v[48:49] neg_lo:[0,1] neg_hi:[0,1]
	v_pk_add_f32 v[48:49], v[40:41], v[42:43]
	v_pk_add_f32 v[40:41], v[40:41], v[42:43] neg_lo:[0,1] neg_hi:[0,1]
	v_pk_add_f32 v[42:43], v[28:29], v[38:39]
	v_pk_add_f32 v[28:29], v[28:29], v[38:39] neg_lo:[0,1] neg_hi:[0,1]
	v_pk_add_f32 v[36:37], v[46:47], v[78:79] neg_lo:[0,1] neg_hi:[0,1]
	v_xor_b32_e32 v38, 0x80000000, v29
	v_mov_b32_e32 v39, v28
	v_pk_add_f32 v[28:29], v[48:49], v[42:43]
	v_pk_add_f32 v[42:43], v[48:49], v[42:43] neg_lo:[0,1] neg_hi:[0,1]
	v_pk_add_f32 v[48:49], v[40:41], v[38:39]
	v_pk_add_f32 v[38:39], v[40:41], v[38:39] neg_lo:[0,1] neg_hi:[0,1]
	v_pk_add_f32 v[40:41], v[16:17], v[44:45]
	v_pk_add_f32 v[16:17], v[16:17], v[44:45] neg_lo:[0,1] neg_hi:[0,1]
	v_pk_add_f32 v[44:45], v[18:19], v[26:27]
	v_pk_add_f32 v[18:19], v[18:19], v[26:27] neg_lo:[0,1] neg_hi:[0,1]
	s_nop 0
	v_xor_b32_e32 v26, 0x80000000, v19
	v_mov_b32_e32 v27, v18
	v_pk_mul_f32 v[26:27], v[10:11], v[26:27] op_sel_hi:[0,1]
	v_pk_fma_f32 v[18:19], v[10:11], v[18:19], v[26:27] op_sel_hi:[0,1,1]
	v_pk_add_f32 v[26:27], v[22:23], v[30:31]
	v_pk_add_f32 v[22:23], v[22:23], v[30:31] neg_lo:[0,1] neg_hi:[0,1]
	s_nop 0
	v_xor_b32_e32 v30, 0x80000000, v23
	v_mov_b32_e32 v31, v22
	v_pk_add_f32 v[22:23], v[24:25], v[20:21]
	v_pk_add_f32 v[20:21], v[24:25], v[20:21] neg_lo:[0,1] neg_hi:[0,1]
	s_nop 0
	v_xor_b32_e32 v24, 0x80000000, v21
	v_mov_b32_e32 v25, v20
	v_pk_mul_f32 v[24:25], v[10:11], v[24:25] op_sel_hi:[0,1]
	v_pk_fma_f32 v[20:21], v[10:11], v[20:21], v[24:25] op_sel_hi:[0,1,1] neg_lo:[1,0,0] neg_hi:[1,0,0]
	v_pk_add_f32 v[24:25], v[40:41], v[26:27]
	v_pk_add_f32 v[26:27], v[40:41], v[26:27] neg_lo:[0,1] neg_hi:[0,1]
	v_pk_add_f32 v[40:41], v[44:45], v[22:23]
	v_pk_add_f32 v[22:23], v[44:45], v[22:23] neg_lo:[0,1] neg_hi:[0,1]
	s_nop 0
	v_xor_b32_e32 v44, 0x80000000, v23
	v_mov_b32_e32 v45, v22
	v_pk_add_f32 v[22:23], v[24:25], v[40:41]
	v_pk_add_f32 v[24:25], v[24:25], v[40:41] neg_lo:[0,1] neg_hi:[0,1]
	v_pk_add_f32 v[40:41], v[26:27], v[44:45]
	v_pk_add_f32 v[26:27], v[26:27], v[44:45] neg_lo:[0,1] neg_hi:[0,1]
	v_pk_add_f32 v[44:45], v[16:17], v[30:31]
	v_pk_add_f32 v[16:17], v[16:17], v[30:31] neg_lo:[0,1] neg_hi:[0,1]
	v_pk_add_f32 v[30:31], v[18:19], v[20:21]
	v_pk_add_f32 v[18:19], v[18:19], v[20:21] neg_lo:[0,1] neg_hi:[0,1]
	s_nop 0
	v_xor_b32_e32 v20, 0x80000000, v19
	v_mov_b32_e32 v21, v18
	v_pk_add_f32 v[18:19], v[44:45], v[30:31]
	v_pk_add_f32 v[30:31], v[44:45], v[30:31] neg_lo:[0,1] neg_hi:[0,1]
	v_pk_add_f32 v[44:45], v[16:17], v[20:21]
	v_pk_add_f32 v[16:17], v[16:17], v[20:21] neg_lo:[0,1] neg_hi:[0,1]
	v_pk_add_f32 v[20:21], v[46:47], v[78:79]
	ds_write2_b64 v13, v[52:53], v[20:21] offset1:16
	ds_write2_b64 v15, v[70:71], v[22:23] offset0:32 offset1:48
	ds_write2_b64 v51, v[74:75], v[28:29] offset0:64 offset1:80
	ds_write2_b64 v54, v[34:35], v[18:19] offset0:96 offset1:112
	ds_write2_b64 v55, v[94:95], v[86:87] offset0:128 offset1:144
	ds_write2_b64 v56, v[88:89], v[40:41] offset0:160 offset1:176
	ds_write2_b64 v57, v[96:97], v[48:49] offset0:192 offset1:208
	ds_write2_b64 v58, v[84:85], v[44:45] offset0:224 offset1:240
	ds_write2_b64 v59, v[92:93], v[36:37] offset1:16
	ds_write2_b64 v60, v[72:73], v[24:25] offset0:32 offset1:48
	ds_write2_b64 v61, v[90:91], v[42:43] offset0:64 offset1:80
	ds_write2_b64 v62, v[82:83], v[30:31] offset0:96 offset1:112
	ds_write2_b64 v63, v[80:81], v[32:33] offset0:128 offset1:144
	ds_write2_b64 v64, v[76:77], v[26:27] offset0:160 offset1:176
	ds_write2_b64 v65, v[68:69], v[38:39] offset0:192 offset1:208
	ds_write2_b64 v101, v[66:67], v[16:17] offset0:224 offset1:240
	v_mov_b32_e32 v10, v173
	s_waitcnt lgkmcnt(0)
	s_barrier
	v_mov_b32_e32 v58, v178
	v_mov_b32_e32 v59, v179
	v_lshl_add_u32 v10, v10, 3, 0
	ds_read_b64 v[34:35], v10
	ds_read_b64 v[36:37], v10 offset:4224
	ds_read_b64 v[38:39], v10 offset:8448
	ds_read_b64 v[40:41], v10 offset:12672
	ds_read_b64 v[42:43], v10 offset:16896
	ds_read_b64 v[44:45], v10 offset:21120
	ds_read_b64 v[50:51], v10 offset:25344
	ds_read_b64 v[52:53], v10 offset:29568
	ds_read_b64 v[54:55], v10 offset:33792
	ds_read_b64 v[56:57], v10 offset:38016
	ds_read_b64 v[64:65], v10 offset:42240
	ds_read_b64 v[74:75], v10 offset:46464
	ds_read_b64 v[76:77], v10 offset:50688
	ds_read_b64 v[78:79], v10 offset:54912
	ds_read_b64 v[80:81], v10 offset:59136
	ds_read_b64 v[82:83], v10 offset:63360
	v_add_u32_e32 v13, 0x10800, v10
	v_add_u32_e32 v15, 0x11880, v10
	v_add_u32_e32 v16, 0x12900, v10
	v_add_u32_e32 v17, 0x13980, v10
	ds_read_b64 v[84:85], v13
	ds_read_b64 v[86:87], v15
	ds_read_b64 v[88:89], v16
	ds_read_b64 v[92:93], v17
	v_add_u32_e32 v13, 0x14a00, v10
	v_add_u32_e32 v15, 0x15a80, v10
	v_add_u32_e32 v16, 0x16b00, v10
	v_add_u32_e32 v17, 0x17b80, v10
	ds_read_b64 v[96:97], v13
	ds_read_b64 v[98:99], v15
	ds_read_b64 v[94:95], v16
	ds_read_b64 v[90:91], v17
	v_add_u32_e32 v13, 0x18c00, v10
	v_add_u32_e32 v15, 0x19c80, v10
	v_add_u32_e32 v16, 0x1ad00, v10
	v_add_u32_e32 v17, 0x1bd80, v10
	ds_read_b64 v[72:73], v13
	ds_read_b64 v[70:71], v15
	ds_read_b64 v[68:69], v16
	ds_read_b64 v[66:67], v17
	v_add_u32_e32 v13, 0x1ce00, v10
	v_add_u32_e32 v15, 0x1de80, v10
	v_add_u32_e32 v16, 0x1ef00, v10
	v_add_u32_e32 v10, 0x1ff80, v10
	ds_read_b64 v[62:63], v13
	ds_read_b64 v[60:61], v15
	ds_read_b64 v[100:101], v16
	ds_read_b64 v[102:103], v10
	s_mov_b32 s43, s95
	v_mov_b32_e32 v10, v1
	s_lshl_b64 s[0:1], s[42:43], 2
	v_readlane_b32 s2, v251, 46
	s_add_u32 s0, s2, s0
	v_readlane_b32 s2, v251, 48
	v_readlane_b32 s6, v251, 52
	v_mov_b32_e32 v24, v164
	v_mov_b32_e32 v32, v165
	v_mov_b32_e32 v28, v166
	v_mov_b32_e32 v46, v167
	v_mov_b32_e32 v48, v168
	v_mov_b32_e32 v30, v169
	v_mov_b32_e32 v26, v170
	v_mov_b32_e32 v10, v171
	v_mov_b32_e32 v16, v183
	v_mov_b32_e32 v19, v184
	s_addc_u32 s1, s2, s1
	v_readlane_b32 s7, v251, 53
	s_waitcnt lgkmcnt(0)
	s_barrier
	global_load_dword v13, v11, s[0:1]
	s_and_b64 s[0:1], s[6:7], exec
	s_movk_i32 s0, 0x800
	s_cselect_b32 s2, 0x400, s0
	v_readlane_b32 s24, v251, 50
	s_add_i32 s4, s2, s24
	s_mul_i32 s0, s4, 0x8200
	v_readlane_b32 s3, v251, 18
	s_mul_hi_i32 s1, s4, 0x8200
	s_add_u32 s0, s3, s0
	v_readlane_b32 s3, v251, 20
	s_addc_u32 s1, s3, s1
	s_lshl_b32 s2, s2, 2
	v_mov_b32_e32 v10, s2
	v_readlane_b32 s2, v251, 42
	v_readlane_b32 s3, v251, 43
	v_readlane_b32 s8, v250, 23
	v_readlane_b32 s9, v250, 24
	v_ashrrev_i32_e32 v15, 31, v14
	v_lshl_add_u64 v[22:23], v[14:15], 2, s[70:71]
	v_readlane_b32 s22, v250, 37
	global_load_dword v197, v10, s[2:3]
	s_add_i32 s2, s4, 0xc00
	s_ashr_i32 s3, s2, 31
	s_lshl_b64 s[2:3], s[2:3], 2
	s_add_u32 s2, s8, s2
	s_addc_u32 s3, s9, s3
	global_load_dword v198, v11, s[2:3]
	s_add_i32 s2, s4, 0x1800
	s_ashr_i32 s3, s2, 31
	s_lshl_b64 s[2:3], s[2:3], 2
	s_add_u32 s2, s8, s2
	s_addc_u32 s3, s9, s3
	global_load_dword v199, v11, s[2:3]
	v_readlane_b32 s2, v251, 40
	v_readlane_b32 s3, v251, 41
	v_cmp_lt_i32_e32 vcc, 0, v14
	v_mov_b32_e32 v17, 0
	v_lshl_add_u64 v[20:21], v[14:15], 1, s[0:1]
	v_mov_b32_e32 v18, 0
	v_readlane_b32 s25, v251, 51
	global_load_dword v200, v10, s[2:3]
	v_readlane_b32 s10, v250, 25
	v_lshlrev_b32_e32 v241, 1, v14
	v_lshlrev_b32_e32 v242, 2, v14
	v_add_u32_e32 v242, 0x1000, v242
	global_load_dword v190, v242, s[70:71] offset:-4096
	global_load_ushort v202, v241, s[0:1] offset:-2
	global_load_ushort v203, v241, s[0:1]
	global_load_ushort v204, v241, s[0:1] offset:2
	global_load_dword v205, v242, s[64:65] offset:-4096
	global_load_dword v206, v242, s[70:71] offset:-2048
	global_load_ushort v207, v241, s[0:1] offset:1022
	global_load_ushort v208, v241, s[0:1] offset:1024
	global_load_ushort v209, v241, s[0:1] offset:1026
	global_load_dword v210, v242, s[64:65] offset:-2048
	global_load_dword v211, v242, s[70:71]
	global_load_ushort v212, v241, s[0:1] offset:2046
	global_load_ushort v213, v241, s[0:1] offset:2048
	global_load_ushort v214, v241, s[0:1] offset:2050
	global_load_dword v215, v242, s[64:65]
	global_load_dword v216, v242, s[70:71] offset:2048
	global_load_ushort v217, v241, s[0:1] offset:3070
	global_load_ushort v218, v241, s[0:1] offset:3072
	global_load_ushort v219, v241, s[0:1] offset:3074
	global_load_dword v220, v242, s[64:65] offset:2048
	v_lshlrev_b32_e32 v241, 1, v14
	v_add_u32_e32 v241, 0x1000, v241
	v_lshlrev_b32_e32 v242, 2, v14
	v_add_u32_e32 v242, 0x3000, v242
	global_load_dword v221, v242, s[70:71] offset:-4096
	global_load_ushort v222, v241, s[0:1] offset:-2
	global_load_ushort v223, v241, s[0:1]
	global_load_ushort v224, v241, s[0:1] offset:2
	global_load_dword v225, v242, s[64:65] offset:-4096
	global_load_dword v226, v242, s[70:71] offset:-2048
	global_load_ushort v227, v241, s[0:1] offset:1022
	global_load_ushort v228, v241, s[0:1] offset:1024
	global_load_ushort v229, v241, s[0:1] offset:1026
	global_load_dword v230, v242, s[64:65] offset:-2048
	global_load_dword v231, v242, s[70:71]
	global_load_ushort v232, v241, s[0:1] offset:2046
	global_load_ushort v233, v241, s[0:1] offset:2048
	global_load_ushort v234, v241, s[0:1] offset:2050
	global_load_dword v235, v242, s[64:65]
	global_load_dword v236, v242, s[70:71] offset:2048
	global_load_ushort v237, v241, s[0:1] offset:3070
	global_load_ushort v238, v241, s[0:1] offset:3072
	global_load_ushort v239, v241, s[0:1] offset:3074
	global_load_dword v240, v242, s[64:65] offset:2048
	s_waitcnt vmcnt(20)
	v_mov_b32_e32 v10, v190
	v_readlane_b32 s11, v250, 26
	v_readlane_b32 s12, v250, 27
	v_readlane_b32 s13, v250, 28
	v_readlane_b32 s14, v250, 29
	v_readlane_b32 s15, v250, 30
	v_readlane_b32 s16, v250, 31
	v_readlane_b32 s17, v250, 32
	v_readlane_b32 s18, v250, 33
	v_readlane_b32 s19, v250, 34
	v_readlane_b32 s20, v250, 35
	v_readlane_b32 s21, v250, 36
	v_readlane_b32 s23, v250, 38
	s_and_saveexec_b64 s[2:3], vcc
	s_movk_i32 s22, 0x3fff
	s_cbranch_execz .LBB0_636
	v_mov_b32_e32 v18, v202
	s_nop 0
	v_lshlrev_b32_e32 v18, 16, v18

.LBB0_1199:
	ds_read_b128 v[142:145], v158
	ds_read_b128 v[162:165], v158 offset:1024
	ds_read_b128 v[166:169], v158 offset:2048
	ds_read_b128 v[170:173], v158 offset:3072
	s_add_u32 s26, s24, 0xfffc0080
	s_addc_u32 s27, s25, -1
	s_cmp_eq_u32 s56, 12
	s_cselect_b32 s29, s17, s27
	s_cselect_b32 s28, s52, s26
	s_cselect_b32 s27, s15, s55
	s_cselect_b32 s26, s53, s54
	v_lshl_add_u64 v[146:147], s[24:25], 0, v[134:135]
	s_add_i32 m0, s23, 0xc000
	ds_read_b128 v[174:177], v159
	ds_read_b128 v[178:181], v159 offset:1024
	ds_read_b128 v[182:185], v159 offset:2048
	ds_read_b128 v[186:189], v159 offset:3072
	ds_read_b128 v[192:195], v159 offset:4096
	ds_read_b128 v[196:199], v159 offset:5120
	ds_read_b128 v[200:203], v159 offset:6144
	ds_read_b128 v[204:207], v159 offset:7168
	global_load_lds_dwordx4 v[146:147], off
	v_lshl_add_u64 v[146:147], s[24:25], 0, v[136:137]
	s_add_i32 m0, s23, 0xe000
	s_nop 0
	global_load_lds_dwordx4 v[146:147], off
	s_waitcnt lgkmcnt(8)
	s_barrier
	s_waitcnt lgkmcnt(0)
	s_setprio 1
	s_waitcnt lgkmcnt(0)
	v_mfma_f32_16x16x32_bf16 v[126:129], v[142:145], v[174:177], v[126:129]
	v_mfma_f32_16x16x32_bf16 v[122:125], v[166:169], v[174:177], v[122:125]
	v_mfma_f32_16x16x32_bf16 v[114:117], v[142:145], v[182:185], v[114:117]
	v_mfma_f32_16x16x32_bf16 v[106:109], v[166:169], v[182:185], v[106:109]
	v_mfma_f32_16x16x32_bf16 v[98:101], v[142:145], v[192:195], v[98:101]
	v_mfma_f32_16x16x32_bf16 v[90:93], v[166:169], v[192:195], v[90:93]
	v_mfma_f32_16x16x32_bf16 v[82:85], v[142:145], v[200:203], v[82:85]
	v_mfma_f32_16x16x32_bf16 v[74:77], v[166:169], v[200:203], v[74:77]
	v_mfma_f32_16x16x32_bf16 v[126:129], v[162:165], v[178:181], v[126:129]
	v_mfma_f32_16x16x32_bf16 v[122:125], v[170:173], v[178:181], v[122:125]
	v_mfma_f32_16x16x32_bf16 v[114:117], v[162:165], v[186:189], v[114:117]
	v_mfma_f32_16x16x32_bf16 v[106:109], v[170:173], v[186:189], v[106:109]
	v_mfma_f32_16x16x32_bf16 v[98:101], v[162:165], v[196:199], v[98:101]
	v_mfma_f32_16x16x32_bf16 v[90:93], v[170:173], v[196:199], v[90:93]
	v_mfma_f32_16x16x32_bf16 v[82:85], v[162:165], v[204:207], v[82:85]
	v_mfma_f32_16x16x32_bf16 v[74:77], v[170:173], v[204:207], v[74:77]
	s_setprio 0
	s_barrier
	s_add_i32 s57, s48, s38
	v_lshl_add_u64 v[146:147], s[26:27], 0, v[130:131]
	s_mov_b32 m0, s57
	ds_read_b128 v[208:211], v160
	ds_read_b128 v[212:215], v160 offset:1024
	ds_read_b128 v[216:219], v160 offset:2048
	ds_read_b128 v[220:223], v160 offset:3072
	global_load_lds_dwordx4 v[146:147], off
	v_lshl_add_u64 v[190:191], s[26:27], 0, v[132:133]
	s_add_i32 m0, s57, 0x2000
	s_nop 0
	global_load_lds_dwordx4 v[190:191], off
	s_barrier
	s_waitcnt lgkmcnt(0)
	s_setprio 1
	s_waitcnt lgkmcnt(0)
	v_mfma_f32_16x16x32_bf16 v[118:121], v[208:211], v[174:177], v[118:121]
	v_mfma_f32_16x16x32_bf16 v[110:113], v[216:219], v[174:177], v[110:113]
	v_mfma_f32_16x16x32_bf16 v[102:105], v[208:211], v[182:185], v[102:105]
	v_mfma_f32_16x16x32_bf16 v[94:97], v[216:219], v[182:185], v[94:97]
	v_mfma_f32_16x16x32_bf16 v[86:89], v[208:211], v[192:195], v[86:89]
	v_mfma_f32_16x16x32_bf16 v[78:81], v[216:219], v[192:195], v[78:81]
	v_mfma_f32_16x16x32_bf16 v[70:73], v[208:211], v[200:203], v[70:73]
	v_mfma_f32_16x16x32_bf16 v[66:69], v[216:219], v[200:203], v[66:69]
	v_mfma_f32_16x16x32_bf16 v[118:121], v[212:215], v[178:181], v[118:121]
	v_mfma_f32_16x16x32_bf16 v[110:113], v[220:223], v[178:181], v[110:113]
	v_mfma_f32_16x16x32_bf16 v[102:105], v[212:215], v[186:189], v[102:105]
	v_mfma_f32_16x16x32_bf16 v[94:97], v[220:223], v[186:189], v[94:97]
	v_mfma_f32_16x16x32_bf16 v[86:89], v[212:215], v[196:199], v[86:89]
	v_mfma_f32_16x16x32_bf16 v[78:81], v[220:223], v[196:199], v[78:81]
	v_mfma_f32_16x16x32_bf16 v[70:73], v[212:215], v[204:207], v[70:73]
	v_mfma_f32_16x16x32_bf16 v[66:69], v[220:223], v[204:207], v[66:69]
	s_setprio 0
	s_mov_b32 m0, s23
	v_lshl_add_u64 v[224:225], s[28:29], 0, v[130:131]
	s_barrier
	ds_read_b128 v[174:177], v159 offset:16384
	ds_read_b128 v[178:181], v159 offset:17408
	ds_read_b128 v[182:185], v159 offset:18432
	ds_read_b128 v[186:189], v159 offset:19456
	ds_read_b128 v[192:195], v159 offset:20480
	ds_read_b128 v[196:199], v159 offset:21504
	ds_read_b128 v[200:203], v159 offset:22528
	ds_read_b128 v[204:207], v159 offset:23552
	global_load_lds_dwordx4 v[224:225], off
	v_lshl_add_u64 v[226:227], s[28:29], 0, v[132:133]
	s_mov_b32 m0, s41
	s_nop 0
	global_load_lds_dwordx4 v[226:227], off
	s_barrier
	s_waitcnt lgkmcnt(0)
	s_setprio 1
	s_waitcnt lgkmcnt(0)
	v_mfma_f32_16x16x32_bf16 v[62:65], v[142:145], v[174:177], v[62:65]
	v_mfma_f32_16x16x32_bf16 v[58:61], v[166:169], v[174:177], v[58:61]
	v_mfma_f32_16x16x32_bf16 v[50:53], v[142:145], v[182:185], v[50:53]
	v_mfma_f32_16x16x32_bf16 v[42:45], v[166:169], v[182:185], v[42:45]
	v_mfma_f32_16x16x32_bf16 v[34:37], v[142:145], v[192:195], v[34:37]
	v_mfma_f32_16x16x32_bf16 v[26:29], v[166:169], v[192:195], v[26:29]
	v_mfma_f32_16x16x32_bf16 v[18:21], v[142:145], v[200:203], v[18:21]
	v_mfma_f32_16x16x32_bf16 v[10:13], v[166:169], v[200:203], v[10:13]
	v_mfma_f32_16x16x32_bf16 v[62:65], v[162:165], v[178:181], v[62:65]
	v_mfma_f32_16x16x32_bf16 v[58:61], v[170:173], v[178:181], v[58:61]
	v_mfma_f32_16x16x32_bf16 v[50:53], v[162:165], v[186:189], v[50:53]
	v_mfma_f32_16x16x32_bf16 v[42:45], v[170:173], v[186:189], v[42:45]
	v_mfma_f32_16x16x32_bf16 v[34:37], v[162:165], v[196:199], v[34:37]
	v_mfma_f32_16x16x32_bf16 v[26:29], v[170:173], v[196:199], v[26:29]
	v_mfma_f32_16x16x32_bf16 v[18:21], v[162:165], v[204:207], v[18:21]
	v_mfma_f32_16x16x32_bf16 v[10:13], v[170:173], v[204:207], v[10:13]
	s_setprio 0
	s_barrier
	s_add_u32 s58, s26, 0x40000
	s_addc_u32 s59, s27, 0
	s_add_i32 s57, s49, s38
	v_lshl_add_u64 v[142:143], s[58:59], 0, v[130:131]
	s_mov_b32 m0, s57
	s_nop 0
	global_load_lds_dwordx4 v[142:143], off
	v_lshl_add_u64 v[142:143], s[58:59], 0, v[132:133]
	s_add_i32 m0, s57, 0x2000
	s_nop 0
	global_load_lds_dwordx4 v[142:143], off
	s_waitcnt vmcnt(6)
	s_barrier
	s_setprio 1
	v_mfma_f32_16x16x32_bf16 v[54:57], v[208:211], v[174:177], v[54:57]
	v_mfma_f32_16x16x32_bf16 v[46:49], v[216:219], v[174:177], v[46:49]
	v_mfma_f32_16x16x32_bf16 v[38:41], v[208:211], v[182:185], v[38:41]
	v_mfma_f32_16x16x32_bf16 v[30:33], v[216:219], v[182:185], v[30:33]
	v_mfma_f32_16x16x32_bf16 v[22:25], v[208:211], v[192:195], v[22:25]
	v_mfma_f32_16x16x32_bf16 v[14:17], v[216:219], v[192:195], v[14:17]
	v_mfma_f32_16x16x32_bf16 v[6:9], v[208:211], v[200:203], v[6:9]
	v_mfma_f32_16x16x32_bf16 v[2:5], v[216:219], v[200:203], v[2:5]
	v_mfma_f32_16x16x32_bf16 v[54:57], v[212:215], v[178:181], v[54:57]
	v_mfma_f32_16x16x32_bf16 v[46:49], v[220:223], v[178:181], v[46:49]
	v_mfma_f32_16x16x32_bf16 v[38:41], v[212:215], v[186:189], v[38:41]
	v_mfma_f32_16x16x32_bf16 v[30:33], v[220:223], v[186:189], v[30:33]
	v_mfma_f32_16x16x32_bf16 v[22:25], v[212:215], v[196:199], v[22:25]
	v_mfma_f32_16x16x32_bf16 v[14:17], v[220:223], v[196:199], v[14:17]
	v_mfma_f32_16x16x32_bf16 v[6:9], v[212:215], v[204:207], v[6:9]
	v_mfma_f32_16x16x32_bf16 v[2:5], v[220:223], v[204:207], v[2:5]
	s_setprio 0
	s_add_i32 s57, 0, 0x18000
	v_add_u32_e32 v161, s57, v156
	s_barrier
	ds_read_b128 v[142:145], v161
	ds_read_b128 v[162:165], v161 offset:1024
	ds_read_b128 v[166:169], v161 offset:2048
	ds_read_b128 v[170:173], v161 offset:3072
	s_add_u32 s28, s28, 0x40000
	s_addc_u32 s29, s29, 0
	s_mov_b32 m0, s42
	v_lshl_add_u64 v[208:209], s[28:29], 0, v[130:131]
	ds_read_b128 v[174:177], v159 offset:32768
	ds_read_b128 v[178:181], v159 offset:33792
	ds_read_b128 v[182:185], v159 offset:34816
	ds_read_b128 v[186:189], v159 offset:35840
	ds_read_b128 v[192:195], v159 offset:36864
	ds_read_b128 v[196:199], v159 offset:37888
	ds_read_b128 v[200:203], v159 offset:38912
	ds_read_b128 v[204:207], v159 offset:39936
	global_load_lds_dwordx4 v[208:209], off
	v_lshl_add_u64 v[208:209], s[28:29], 0, v[132:133]
	s_mov_b32 m0, s43
	s_nop 0
	global_load_lds_dwordx4 v[208:209], off
	s_waitcnt lgkmcnt(8)
	s_barrier
	s_waitcnt lgkmcnt(0)
	s_setprio 1
	s_waitcnt lgkmcnt(0)
	v_mfma_f32_16x16x32_bf16 v[126:129], v[142:145], v[174:177], v[126:129]
	v_mfma_f32_16x16x32_bf16 v[122:125], v[166:169], v[174:177], v[122:125]
	v_mfma_f32_16x16x32_bf16 v[114:117], v[142:145], v[182:185], v[114:117]
	v_mfma_f32_16x16x32_bf16 v[106:109], v[166:169], v[182:185], v[106:109]
	v_mfma_f32_16x16x32_bf16 v[98:101], v[142:145], v[192:195], v[98:101]
	v_mfma_f32_16x16x32_bf16 v[90:93], v[166:169], v[192:195], v[90:93]
	v_mfma_f32_16x16x32_bf16 v[82:85], v[142:145], v[200:203], v[82:85]
	v_mfma_f32_16x16x32_bf16 v[74:77], v[166:169], v[200:203], v[74:77]
	v_mfma_f32_16x16x32_bf16 v[126:129], v[162:165], v[178:181], v[126:129]
	v_mfma_f32_16x16x32_bf16 v[122:125], v[170:173], v[178:181], v[122:125]
	v_mfma_f32_16x16x32_bf16 v[114:117], v[162:165], v[186:189], v[114:117]
	v_mfma_f32_16x16x32_bf16 v[106:109], v[170:173], v[186:189], v[106:109]
	v_mfma_f32_16x16x32_bf16 v[98:101], v[162:165], v[196:199], v[98:101]
	v_mfma_f32_16x16x32_bf16 v[90:93], v[170:173], v[196:199], v[90:93]
	v_mfma_f32_16x16x32_bf16 v[82:85], v[162:165], v[204:207], v[82:85]
	v_mfma_f32_16x16x32_bf16 v[74:77], v[170:173], v[204:207], v[74:77]
	s_setprio 0
	s_barrier
	s_add_i32 s28, 0, 0x1c000
	s_add_i32 s29, s57, s38
	v_add_u32_e32 v161, s28, v156
	v_lshl_add_u64 v[146:147], v[146:147], 0, s[8:9]
	s_mov_b32 m0, s29
	ds_read_b128 v[208:211], v161
	ds_read_b128 v[212:215], v161 offset:1024
	ds_read_b128 v[216:219], v161 offset:2048
	ds_read_b128 v[220:223], v161 offset:3072
	global_load_lds_dwordx4 v[146:147], off
	v_lshl_add_u64 v[146:147], v[190:191], 0, s[8:9]
	s_add_i32 m0, s29, 0x2000
	s_nop 0
	global_load_lds_dwordx4 v[146:147], off
	s_barrier
	s_waitcnt lgkmcnt(0)
	s_setprio 1
	s_waitcnt lgkmcnt(0)
	v_mfma_f32_16x16x32_bf16 v[118:121], v[208:211], v[174:177], v[118:121]
	v_mfma_f32_16x16x32_bf16 v[110:113], v[216:219], v[174:177], v[110:113]
	v_mfma_f32_16x16x32_bf16 v[102:105], v[208:211], v[182:185], v[102:105]
	v_mfma_f32_16x16x32_bf16 v[94:97], v[216:219], v[182:185], v[94:97]
	v_mfma_f32_16x16x32_bf16 v[86:89], v[208:211], v[192:195], v[86:89]
	v_mfma_f32_16x16x32_bf16 v[78:81], v[216:219], v[192:195], v[78:81]
	v_mfma_f32_16x16x32_bf16 v[70:73], v[208:211], v[200:203], v[70:73]
	v_mfma_f32_16x16x32_bf16 v[66:69], v[216:219], v[200:203], v[66:69]
	v_mfma_f32_16x16x32_bf16 v[118:121], v[212:215], v[178:181], v[118:121]
	v_mfma_f32_16x16x32_bf16 v[110:113], v[220:223], v[178:181], v[110:113]
	v_mfma_f32_16x16x32_bf16 v[102:105], v[212:215], v[186:189], v[102:105]
	v_mfma_f32_16x16x32_bf16 v[94:97], v[220:223], v[186:189], v[94:97]
	v_mfma_f32_16x16x32_bf16 v[86:89], v[212:215], v[196:199], v[86:89]
	v_mfma_f32_16x16x32_bf16 v[78:81], v[220:223], v[196:199], v[78:81]
	v_mfma_f32_16x16x32_bf16 v[70:73], v[212:215], v[204:207], v[70:73]
	v_mfma_f32_16x16x32_bf16 v[66:69], v[220:223], v[204:207], v[66:69]
	s_setprio 0
	s_mov_b32 m0, s45
	v_lshl_add_u64 v[146:147], v[224:225], 0, s[8:9]
	s_barrier
	ds_read_b128 v[174:177], v159 offset:49152
	ds_read_b128 v[178:181], v159 offset:50176
	ds_read_b128 v[182:185], v159 offset:51200
	ds_read_b128 v[186:189], v159 offset:52224
	ds_read_b128 v[192:195], v159 offset:53248
	ds_read_b128 v[196:199], v159 offset:54272
	ds_read_b128 v[200:203], v159 offset:55296
	ds_read_b128 v[204:207], v159 offset:56320
	global_load_lds_dwordx4 v[146:147], off
	v_lshl_add_u64 v[146:147], v[226:227], 0, s[8:9]
	s_mov_b32 m0, s46
	s_nop 0
	global_load_lds_dwordx4 v[146:147], off
	s_barrier
	s_waitcnt lgkmcnt(0)
	s_setprio 1
	s_waitcnt lgkmcnt(0)
	v_mfma_f32_16x16x32_bf16 v[62:65], v[142:145], v[174:177], v[62:65]
	v_mfma_f32_16x16x32_bf16 v[58:61], v[166:169], v[174:177], v[58:61]
	v_mfma_f32_16x16x32_bf16 v[50:53], v[142:145], v[182:185], v[50:53]
	v_mfma_f32_16x16x32_bf16 v[42:45], v[166:169], v[182:185], v[42:45]
	v_mfma_f32_16x16x32_bf16 v[34:37], v[142:145], v[192:195], v[34:37]
	v_mfma_f32_16x16x32_bf16 v[26:29], v[166:169], v[192:195], v[26:29]
	v_mfma_f32_16x16x32_bf16 v[18:21], v[142:145], v[200:203], v[18:21]
	v_mfma_f32_16x16x32_bf16 v[10:13], v[166:169], v[200:203], v[10:13]
	v_mfma_f32_16x16x32_bf16 v[62:65], v[162:165], v[178:181], v[62:65]
	v_mfma_f32_16x16x32_bf16 v[58:61], v[170:173], v[178:181], v[58:61]
	v_mfma_f32_16x16x32_bf16 v[50:53], v[162:165], v[186:189], v[50:53]
	v_mfma_f32_16x16x32_bf16 v[42:45], v[170:173], v[186:189], v[42:45]
	v_mfma_f32_16x16x32_bf16 v[34:37], v[162:165], v[196:199], v[34:37]
	v_mfma_f32_16x16x32_bf16 v[26:29], v[170:173], v[196:199], v[26:29]
	v_mfma_f32_16x16x32_bf16 v[18:21], v[162:165], v[204:207], v[18:21]
	v_mfma_f32_16x16x32_bf16 v[10:13], v[170:173], v[204:207], v[10:13]
	s_setprio 0
	s_barrier
	s_add_u32 s26, s26, 0x40080
	s_addc_u32 s27, s27, 0
	s_add_i32 s28, s28, s38
	v_lshl_add_u64 v[142:143], s[26:27], 0, v[130:131]
	s_mov_b32 m0, s28
	s_nop 0
	global_load_lds_dwordx4 v[142:143], off
	v_lshl_add_u64 v[142:143], s[26:27], 0, v[132:133]
	s_add_i32 m0, s28, 0x2000
	s_nop 0
	global_load_lds_dwordx4 v[142:143], off
	s_waitcnt vmcnt(6)
	s_barrier
	s_setprio 1
	v_mfma_f32_16x16x32_bf16 v[54:57], v[208:211], v[174:177], v[54:57]
	v_mfma_f32_16x16x32_bf16 v[46:49], v[216:219], v[174:177], v[46:49]
	v_mfma_f32_16x16x32_bf16 v[38:41], v[208:211], v[182:185], v[38:41]
	v_mfma_f32_16x16x32_bf16 v[30:33], v[216:219], v[182:185], v[30:33]
	v_mfma_f32_16x16x32_bf16 v[22:25], v[208:211], v[192:195], v[22:25]
	v_mfma_f32_16x16x32_bf16 v[14:17], v[216:219], v[192:195], v[14:17]
	v_mfma_f32_16x16x32_bf16 v[6:9], v[208:211], v[200:203], v[6:9]
	v_mfma_f32_16x16x32_bf16 v[2:5], v[216:219], v[200:203], v[2:5]
	v_mfma_f32_16x16x32_bf16 v[54:57], v[212:215], v[178:181], v[54:57]
	v_mfma_f32_16x16x32_bf16 v[46:49], v[220:223], v[178:181], v[46:49]
	v_mfma_f32_16x16x32_bf16 v[38:41], v[212:215], v[186:189], v[38:41]
	v_mfma_f32_16x16x32_bf16 v[30:33], v[220:223], v[186:189], v[30:33]
	v_mfma_f32_16x16x32_bf16 v[22:25], v[212:215], v[196:199], v[22:25]
	v_mfma_f32_16x16x32_bf16 v[14:17], v[220:223], v[196:199], v[14:17]
	v_mfma_f32_16x16x32_bf16 v[6:9], v[212:215], v[204:207], v[6:9]
	v_mfma_f32_16x16x32_bf16 v[2:5], v[220:223], v[204:207], v[2:5]
	s_setprio 0
	s_add_i32 s56, s56, 2
	s_add_u32 s24, s24, 0x100
	s_addc_u32 s25, s25, 0
	s_add_u32 s54, s54, 0x100
	s_addc_u32 s55, s55, 0
	s_cmp_gt_u32 s56, 13
	s_barrier
	s_cbranch_scc0 .LBB0_1199
	v_lshl_or_b32 v142, s51, 8, v157
	v_lshl_add_u32 v144, s22, 8, v155
	v_ashrrev_i32_e32 v143, 31, v142
	v_mov_b64_e32 v[146:147], s[10:11]
	v_mad_i64_i32 v[162:163], s[24:25], v144, s50, v[146:147]
	v_lshlrev_b64 v[142:143], 1, v[142:143]
	v_lshl_add_u64 v[162:163], v[162:163], 0, v[142:143]
	v_mov_b32_e32 v238, v162
	v_mov_b32_e32 v239, v163
	global_load_dwordx2 v[168:169], v[238:239], off
	global_load_dwordx2 v[170:171], v[238:239], off offset:32
	global_load_dwordx2 v[172:173], v[238:239], off offset:256
	global_load_dwordx2 v[174:175], v[238:239], off offset:288
	v_mov_b32_e32 v242, 16
	v_mad_i64_i32 v[240:241], s[24:25], v242, s50, v[238:239]
	global_load_dwordx2 v[176:177], v[240:241], off
	global_load_dwordx2 v[178:179], v[240:241], off offset:32
	global_load_dwordx2 v[180:181], v[240:241], off offset:256
	global_load_dwordx2 v[182:183], v[240:241], off offset:288
	v_mov_b32_e32 v242, 32
	v_mad_i64_i32 v[240:241], s[24:25], v242, s50, v[238:239]
	global_load_dwordx2 v[184:185], v[240:241], off
	global_load_dwordx2 v[186:187], v[240:241], off offset:32
	global_load_dwordx2 v[188:189], v[240:241], off offset:256
	global_load_dwordx2 v[192:193], v[240:241], off offset:288
	v_mov_b32_e32 v242, 48
	v_mad_i64_i32 v[240:241], s[24:25], v242, s50, v[238:239]
	global_load_dwordx2 v[194:195], v[240:241], off
	global_load_dwordx2 v[196:197], v[240:241], off offset:32
	global_load_dwordx2 v[198:199], v[240:241], off offset:256
	global_load_dwordx2 v[200:201], v[240:241], off offset:288
	v_mov_b32_e32 v242, 128
	v_mad_i64_i32 v[240:241], s[24:25], v242, s50, v[238:239]
	global_load_dwordx2 v[202:203], v[240:241], off
	global_load_dwordx2 v[204:205], v[240:241], off offset:32
	global_load_dwordx2 v[206:207], v[240:241], off offset:256
	global_load_dwordx2 v[208:209], v[240:241], off offset:288
	v_mov_b32_e32 v242, 144
	v_mad_i64_i32 v[240:241], s[24:25], v242, s50, v[238:239]
	global_load_dwordx2 v[210:211], v[240:241], off
	global_load_dwordx2 v[212:213], v[240:241], off offset:32
	global_load_dwordx2 v[214:215], v[240:241], off offset:256
	global_load_dwordx2 v[216:217], v[240:241], off offset:288
	v_mov_b32_e32 v242, 160
	v_mad_i64_i32 v[240:241], s[24:25], v242, s50, v[238:239]
	global_load_dwordx2 v[218:219], v[240:241], off
	global_load_dwordx2 v[220:221], v[240:241], off offset:32
	global_load_dwordx2 v[222:223], v[240:241], off offset:256
	global_load_dwordx2 v[228:229], v[240:241], off offset:288
	v_mov_b32_e32 v242, 176
	v_mad_i64_i32 v[240:241], s[24:25], v242, s50, v[238:239]
	global_load_dwordx2 v[230:231], v[240:241], off
	global_load_dwordx2 v[232:233], v[240:241], off offset:32
	global_load_dwordx2 v[234:235], v[240:241], off offset:256
	global_load_dwordx2 v[236:237], v[240:241], off offset:288
	s_waitcnt vmcnt(0)
	v_mov_b32_e32 v164, v168
	v_mov_b32_e32 v165, v169
	v_ashrrev_i32_e32 v145, 31, v144
	s_and_b64 vcc, exec, s[0:1]
	s_mov_b32 s51, s14
	s_mov_b32 s22, s16
	s_mov_b64 s[26:27], s[20:21]
	s_nop 0
	v_lshlrev_b32_e32 v166, 16, v164
	v_and_b32_e32 v167, 0xffff0000, v164
	v_lshlrev_b32_e32 v164, 16, v165
	v_and_b32_e32 v165, 0xffff0000, v165
	v_pk_mul_f32 v[128:129], v[128:129], v[164:165]
	v_pk_mul_f32 v[126:127], v[126:127], v[166:167]
	v_lshlrev_b64 v[164:165], 12, v[144:145]
	v_cvt_pk_bf16_f32 v126, v126, v127
	v_cvt_pk_bf16_f32 v127, v128, v129
	v_mov_b32_e32 v128, v170
	v_mov_b32_e32 v129, v171
	v_lshl_add_u64 v[164:165], s[12:13], 0, v[164:165]
	v_lshl_add_u64 v[164:165], v[164:165], 0, v[142:143]
	global_store_dwordx2 v[164:165], v[126:127], off
	s_nop 0
	v_lshlrev_b32_e32 v126, 16, v128
	v_and_b32_e32 v127, 0xffff0000, v128
	v_lshlrev_b32_e32 v128, 16, v129
	v_and_b32_e32 v129, 0xffff0000, v129
	v_pk_mul_f32 v[124:125], v[124:125], v[128:129]
	v_pk_mul_f32 v[122:123], v[122:123], v[126:127]
	s_nop 0
	v_cvt_pk_bf16_f32 v122, v122, v123
	v_cvt_pk_bf16_f32 v123, v124, v125
	v_mov_b32_e32 v124, v172
	v_mov_b32_e32 v125, v173
	s_nop 0
	global_store_dwordx2 v[164:165], v[122:123], off offset:32
	s_nop 0
	v_lshlrev_b32_e32 v122, 16, v124
	v_and_b32_e32 v123, 0xffff0000, v124
	v_lshlrev_b32_e32 v124, 16, v125
	v_and_b32_e32 v125, 0xffff0000, v125
	v_pk_mul_f32 v[120:121], v[120:121], v[124:125]
	v_pk_mul_f32 v[118:119], v[118:119], v[122:123]
	v_or_b32_e32 v122, 16, v144
	v_cvt_pk_bf16_f32 v118, v118, v119
	v_cvt_pk_bf16_f32 v119, v120, v121
	v_mov_b32_e32 v120, v174
	v_mov_b32_e32 v121, v175
	v_mad_i64_i32 v[124:125], s[24:25], v122, s50, v[146:147]
	global_store_dwordx2 v[164:165], v[118:119], off offset:256
	v_lshl_add_u64 v[124:125], v[124:125], 0, v[142:143]
	v_ashrrev_i32_e32 v123, 31, v122
	s_nop 0
	v_lshlrev_b32_e32 v118, 16, v120
	v_and_b32_e32 v119, 0xffff0000, v120
	v_lshlrev_b32_e32 v120, 16, v121
	v_and_b32_e32 v121, 0xffff0000, v121
	v_pk_mul_f32 v[112:113], v[112:113], v[120:121]
	v_pk_mul_f32 v[110:111], v[110:111], v[118:119]
	s_nop 0
	v_cvt_pk_bf16_f32 v110, v110, v111
	v_cvt_pk_bf16_f32 v111, v112, v113
	v_mov_b32_e32 v112, v176
	v_mov_b32_e32 v113, v177
	s_nop 0
	global_store_dwordx2 v[164:165], v[110:111], off offset:288
	s_nop 0
	v_lshlrev_b32_e32 v110, 16, v112
	v_and_b32_e32 v111, 0xffff0000, v112
	v_lshlrev_b32_e32 v112, 16, v113
	v_and_b32_e32 v113, 0xffff0000, v113
	v_pk_mul_f32 v[112:113], v[116:117], v[112:113]
	v_pk_mul_f32 v[110:111], v[114:115], v[110:111]
	v_lshlrev_b64 v[114:115], 12, v[122:123]
	v_cvt_pk_bf16_f32 v110, v110, v111
	v_cvt_pk_bf16_f32 v111, v112, v113
	v_mov_b32_e32 v112, v178
	v_mov_b32_e32 v113, v179
	v_lshl_add_u64 v[114:115], s[12:13], 0, v[114:115]
	v_lshl_add_u64 v[114:115], v[114:115], 0, v[142:143]
	global_store_dwordx2 v[114:115], v[110:111], off
	s_nop 0
	v_lshlrev_b32_e32 v110, 16, v112
	v_and_b32_e32 v111, 0xffff0000, v112
	v_lshlrev_b32_e32 v112, 16, v113
	v_and_b32_e32 v113, 0xffff0000, v113
	v_pk_mul_f32 v[108:109], v[108:109], v[112:113]
	v_pk_mul_f32 v[106:107], v[106:107], v[110:111]
	s_nop 0
	v_cvt_pk_bf16_f32 v106, v106, v107
	v_cvt_pk_bf16_f32 v107, v108, v109
	v_mov_b32_e32 v108, v180
	v_mov_b32_e32 v109, v181
	s_nop 0
	global_store_dwordx2 v[114:115], v[106:107], off offset:32
	s_nop 0
	v_lshlrev_b32_e32 v106, 16, v108
	v_and_b32_e32 v107, 0xffff0000, v108
	v_lshlrev_b32_e32 v108, 16, v109
	v_and_b32_e32 v109, 0xffff0000, v109
	v_pk_mul_f32 v[104:105], v[104:105], v[108:109]
	v_pk_mul_f32 v[102:103], v[102:103], v[106:107]
	v_or_b32_e32 v106, 32, v144
	v_cvt_pk_bf16_f32 v102, v102, v103
	v_cvt_pk_bf16_f32 v103, v104, v105
	v_mov_b32_e32 v104, v182
	v_mov_b32_e32 v105, v183
	v_mad_i64_i32 v[108:109], s[24:25], v106, s50, v[146:147]
	global_store_dwordx2 v[114:115], v[102:103], off offset:256
	v_lshl_add_u64 v[108:109], v[108:109], 0, v[142:143]
	v_ashrrev_i32_e32 v107, 31, v106
	s_nop 0
	v_lshlrev_b32_e32 v102, 16, v104
	v_and_b32_e32 v103, 0xffff0000, v104
	v_lshlrev_b32_e32 v104, 16, v105
	v_and_b32_e32 v105, 0xffff0000, v105
	v_pk_mul_f32 v[96:97], v[96:97], v[104:105]
	v_pk_mul_f32 v[94:95], v[94:95], v[102:103]
	s_nop 0
	v_cvt_pk_bf16_f32 v94, v94, v95
	v_cvt_pk_bf16_f32 v95, v96, v97
	v_mov_b32_e32 v96, v184
	v_mov_b32_e32 v97, v185
	s_nop 0
	global_store_dwordx2 v[114:115], v[94:95], off offset:288
	s_nop 0
	v_lshlrev_b32_e32 v94, 16, v96
	v_and_b32_e32 v95, 0xffff0000, v96
	v_lshlrev_b32_e32 v96, 16, v97
	v_and_b32_e32 v97, 0xffff0000, v97
	v_pk_mul_f32 v[96:97], v[100:101], v[96:97]
	v_pk_mul_f32 v[94:95], v[98:99], v[94:95]
	v_lshlrev_b64 v[98:99], 12, v[106:107]
	v_cvt_pk_bf16_f32 v94, v94, v95
	v_cvt_pk_bf16_f32 v95, v96, v97
	v_mov_b32_e32 v96, v186
	v_mov_b32_e32 v97, v187
	v_lshl_add_u64 v[98:99], s[12:13], 0, v[98:99]
	v_lshl_add_u64 v[98:99], v[98:99], 0, v[142:143]
	global_store_dwordx2 v[98:99], v[94:95], off
	s_nop 0
	v_lshlrev_b32_e32 v94, 16, v96
	v_and_b32_e32 v95, 0xffff0000, v96
	v_lshlrev_b32_e32 v96, 16, v97
	v_and_b32_e32 v97, 0xffff0000, v97
	v_pk_mul_f32 v[92:93], v[92:93], v[96:97]
	v_pk_mul_f32 v[90:91], v[90:91], v[94:95]
	s_nop 0
	v_cvt_pk_bf16_f32 v90, v90, v91
	v_cvt_pk_bf16_f32 v91, v92, v93
	v_mov_b32_e32 v92, v188
	v_mov_b32_e32 v93, v189
	s_nop 0
	global_store_dwordx2 v[98:99], v[90:91], off offset:32
	s_nop 0
	v_lshlrev_b32_e32 v90, 16, v92
	v_and_b32_e32 v91, 0xffff0000, v92
	v_lshlrev_b32_e32 v92, 16, v93
	v_and_b32_e32 v93, 0xffff0000, v93
	v_pk_mul_f32 v[88:89], v[88:89], v[92:93]
	v_pk_mul_f32 v[86:87], v[86:87], v[90:91]
	v_or_b32_e32 v90, 48, v144
	v_cvt_pk_bf16_f32 v86, v86, v87
	v_cvt_pk_bf16_f32 v87, v88, v89
	v_mov_b32_e32 v88, v192
	v_mov_b32_e32 v89, v193
	v_mad_i64_i32 v[92:93], s[24:25], v90, s50, v[146:147]
	global_store_dwordx2 v[98:99], v[86:87], off offset:256
	v_lshl_add_u64 v[92:93], v[92:93], 0, v[142:143]
	v_ashrrev_i32_e32 v91, 31, v90
	s_nop 0
	v_lshlrev_b32_e32 v86, 16, v88
	v_and_b32_e32 v87, 0xffff0000, v88
	v_lshlrev_b32_e32 v88, 16, v89
	v_and_b32_e32 v89, 0xffff0000, v89
	v_pk_mul_f32 v[80:81], v[80:81], v[88:89]
	v_pk_mul_f32 v[78:79], v[78:79], v[86:87]
	s_nop 0
	v_cvt_pk_bf16_f32 v78, v78, v79
	v_cvt_pk_bf16_f32 v79, v80, v81
	v_mov_b32_e32 v80, v194
	v_mov_b32_e32 v81, v195
	s_nop 0
	global_store_dwordx2 v[98:99], v[78:79], off offset:288
	s_nop 0
	v_lshlrev_b32_e32 v78, 16, v80
	v_and_b32_e32 v79, 0xffff0000, v80
	v_lshlrev_b32_e32 v80, 16, v81
	v_and_b32_e32 v81, 0xffff0000, v81
	v_pk_mul_f32 v[80:81], v[84:85], v[80:81]
	v_pk_mul_f32 v[78:79], v[82:83], v[78:79]
	v_lshlrev_b64 v[82:83], 12, v[90:91]
	v_cvt_pk_bf16_f32 v78, v78, v79
	v_cvt_pk_bf16_f32 v79, v80, v81
	v_mov_b32_e32 v80, v196
	v_mov_b32_e32 v81, v197
	v_lshl_add_u64 v[82:83], s[12:13], 0, v[82:83]
	v_lshl_add_u64 v[82:83], v[82:83], 0, v[142:143]
	global_store_dwordx2 v[82:83], v[78:79], off
	s_nop 0
	v_lshlrev_b32_e32 v78, 16, v80
	v_and_b32_e32 v79, 0xffff0000, v80
	v_lshlrev_b32_e32 v80, 16, v81
	v_and_b32_e32 v81, 0xffff0000, v81
	v_pk_mul_f32 v[76:77], v[76:77], v[80:81]
	v_pk_mul_f32 v[74:75], v[74:75], v[78:79]
	s_nop 0
	v_cvt_pk_bf16_f32 v74, v74, v75
	v_cvt_pk_bf16_f32 v75, v76, v77
	v_mov_b32_e32 v76, v198
	v_mov_b32_e32 v77, v199
	s_nop 0
	global_store_dwordx2 v[82:83], v[74:75], off offset:32
	s_nop 0
	v_lshlrev_b32_e32 v74, 16, v76
	v_and_b32_e32 v75, 0xffff0000, v76
	v_lshlrev_b32_e32 v76, 16, v77
	v_and_b32_e32 v77, 0xffff0000, v77
	v_pk_mul_f32 v[72:73], v[72:73], v[76:77]
	v_pk_mul_f32 v[70:71], v[70:71], v[74:75]
	v_add_u32_e32 v74, 0x80, v144
	v_cvt_pk_bf16_f32 v70, v70, v71
	v_cvt_pk_bf16_f32 v71, v72, v73
	v_mov_b32_e32 v72, v200
	v_mov_b32_e32 v73, v201
	v_mad_i64_i32 v[76:77], s[24:25], v74, s50, v[146:147]
	global_store_dwordx2 v[82:83], v[70:71], off offset:256
	v_lshl_add_u64 v[76:77], v[76:77], 0, v[142:143]
	v_ashrrev_i32_e32 v75, 31, v74
	s_nop 0
	v_lshlrev_b32_e32 v70, 16, v72
	v_and_b32_e32 v71, 0xffff0000, v72
	v_lshlrev_b32_e32 v72, 16, v73
	v_and_b32_e32 v73, 0xffff0000, v73
	v_pk_mul_f32 v[68:69], v[68:69], v[72:73]
	v_pk_mul_f32 v[66:67], v[66:67], v[70:71]
	s_nop 0
	v_cvt_pk_bf16_f32 v66, v66, v67
	v_cvt_pk_bf16_f32 v67, v68, v69
	v_mov_b32_e32 v68, v202
	v_mov_b32_e32 v69, v203
	s_nop 0
	global_store_dwordx2 v[82:83], v[66:67], off offset:288
	s_nop 0
	v_lshlrev_b32_e32 v66, 16, v68
	v_and_b32_e32 v67, 0xffff0000, v68
	v_lshlrev_b32_e32 v68, 16, v69
	v_and_b32_e32 v69, 0xffff0000, v69
	v_pk_mul_f32 v[64:65], v[64:65], v[68:69]
	v_pk_mul_f32 v[62:63], v[62:63], v[66:67]
	v_lshlrev_b64 v[66:67], 12, v[74:75]
	v_cvt_pk_bf16_f32 v62, v62, v63
	v_cvt_pk_bf16_f32 v63, v64, v65
	v_mov_b32_e32 v64, v204
	v_mov_b32_e32 v65, v205
	v_lshl_add_u64 v[66:67], s[12:13], 0, v[66:67]
	v_lshl_add_u64 v[66:67], v[66:67], 0, v[142:143]
	global_store_dwordx2 v[66:67], v[62:63], off
	s_nop 0
	v_lshlrev_b32_e32 v62, 16, v64
	v_and_b32_e32 v63, 0xffff0000, v64
	v_lshlrev_b32_e32 v64, 16, v65
	v_and_b32_e32 v65, 0xffff0000, v65
	v_pk_mul_f32 v[60:61], v[60:61], v[64:65]
	v_pk_mul_f32 v[58:59], v[58:59], v[62:63]
	s_nop 0
	v_cvt_pk_bf16_f32 v58, v58, v59
	v_cvt_pk_bf16_f32 v59, v60, v61
	v_mov_b32_e32 v60, v206
	v_mov_b32_e32 v61, v207
	s_nop 0
	global_store_dwordx2 v[66:67], v[58:59], off offset:32
	s_nop 0
	v_lshlrev_b32_e32 v58, 16, v60
	v_and_b32_e32 v59, 0xffff0000, v60
	v_lshlrev_b32_e32 v60, 16, v61
	v_and_b32_e32 v61, 0xffff0000, v61
	v_pk_mul_f32 v[56:57], v[56:57], v[60:61]
	v_pk_mul_f32 v[54:55], v[54:55], v[58:59]
	v_add_u32_e32 v58, 0x90, v144
	v_cvt_pk_bf16_f32 v54, v54, v55
	v_cvt_pk_bf16_f32 v55, v56, v57
	v_mov_b32_e32 v56, v208
	v_mov_b32_e32 v57, v209
	v_mad_i64_i32 v[60:61], s[24:25], v58, s50, v[146:147]
	global_store_dwordx2 v[66:67], v[54:55], off offset:256
	v_lshl_add_u64 v[60:61], v[60:61], 0, v[142:143]
	v_ashrrev_i32_e32 v59, 31, v58
	s_nop 0
	v_lshlrev_b32_e32 v54, 16, v56
	v_and_b32_e32 v55, 0xffff0000, v56
	v_lshlrev_b32_e32 v56, 16, v57
	v_and_b32_e32 v57, 0xffff0000, v57
	v_pk_mul_f32 v[48:49], v[48:49], v[56:57]
	v_pk_mul_f32 v[46:47], v[46:47], v[54:55]
	s_nop 0
	v_cvt_pk_bf16_f32 v46, v46, v47
	v_cvt_pk_bf16_f32 v47, v48, v49
	v_mov_b32_e32 v48, v210
	v_mov_b32_e32 v49, v211
	s_nop 0
	global_store_dwordx2 v[66:67], v[46:47], off offset:288
	s_nop 0
	v_lshlrev_b32_e32 v46, 16, v48
	v_and_b32_e32 v47, 0xffff0000, v48
	v_lshlrev_b32_e32 v48, 16, v49
	v_and_b32_e32 v49, 0xffff0000, v49
	v_pk_mul_f32 v[48:49], v[52:53], v[48:49]
	v_pk_mul_f32 v[46:47], v[50:51], v[46:47]
	v_lshlrev_b64 v[50:51], 12, v[58:59]
	v_cvt_pk_bf16_f32 v46, v46, v47
	v_cvt_pk_bf16_f32 v47, v48, v49
	v_mov_b32_e32 v48, v212
	v_mov_b32_e32 v49, v213
	v_lshl_add_u64 v[50:51], s[12:13], 0, v[50:51]
	v_lshl_add_u64 v[50:51], v[50:51], 0, v[142:143]
	global_store_dwordx2 v[50:51], v[46:47], off
	s_nop 0
	v_lshlrev_b32_e32 v46, 16, v48
	v_and_b32_e32 v47, 0xffff0000, v48
	v_lshlrev_b32_e32 v48, 16, v49
	v_and_b32_e32 v49, 0xffff0000, v49
	v_pk_mul_f32 v[44:45], v[44:45], v[48:49]
	v_pk_mul_f32 v[42:43], v[42:43], v[46:47]
	s_nop 0
	v_cvt_pk_bf16_f32 v42, v42, v43
	v_cvt_pk_bf16_f32 v43, v44, v45
	v_mov_b32_e32 v44, v214
	v_mov_b32_e32 v45, v215
	s_nop 0
	global_store_dwordx2 v[50:51], v[42:43], off offset:32
	s_nop 0
	v_lshlrev_b32_e32 v42, 16, v44
	v_and_b32_e32 v43, 0xffff0000, v44
	v_lshlrev_b32_e32 v44, 16, v45
	v_and_b32_e32 v45, 0xffff0000, v45
	v_pk_mul_f32 v[40:41], v[40:41], v[44:45]
	v_pk_mul_f32 v[38:39], v[38:39], v[42:43]
	v_add_u32_e32 v42, 0xa0, v144
	v_cvt_pk_bf16_f32 v38, v38, v39
	v_cvt_pk_bf16_f32 v39, v40, v41
	v_mov_b32_e32 v40, v216
	v_mov_b32_e32 v41, v217
	v_mad_i64_i32 v[44:45], s[24:25], v42, s50, v[146:147]
	global_store_dwordx2 v[50:51], v[38:39], off offset:256
	v_lshl_add_u64 v[44:45], v[44:45], 0, v[142:143]
	v_ashrrev_i32_e32 v43, 31, v42
	s_nop 0
	v_lshlrev_b32_e32 v38, 16, v40
	v_and_b32_e32 v39, 0xffff0000, v40
	v_lshlrev_b32_e32 v40, 16, v41
	v_and_b32_e32 v41, 0xffff0000, v41
	v_pk_mul_f32 v[32:33], v[32:33], v[40:41]
	v_pk_mul_f32 v[30:31], v[30:31], v[38:39]
	s_nop 0
	v_cvt_pk_bf16_f32 v30, v30, v31
	v_cvt_pk_bf16_f32 v31, v32, v33
	v_mov_b32_e32 v32, v218
	v_mov_b32_e32 v33, v219
	s_nop 0
	global_store_dwordx2 v[50:51], v[30:31], off offset:288
	s_nop 0
	v_lshlrev_b32_e32 v30, 16, v32
	v_and_b32_e32 v31, 0xffff0000, v32
	v_lshlrev_b32_e32 v32, 16, v33
	v_and_b32_e32 v33, 0xffff0000, v33
	v_pk_mul_f32 v[32:33], v[36:37], v[32:33]
	v_pk_mul_f32 v[30:31], v[34:35], v[30:31]
	v_lshlrev_b64 v[34:35], 12, v[42:43]
	v_cvt_pk_bf16_f32 v30, v30, v31
	v_cvt_pk_bf16_f32 v31, v32, v33
	v_mov_b32_e32 v32, v220
	v_mov_b32_e32 v33, v221
	v_lshl_add_u64 v[34:35], s[12:13], 0, v[34:35]
	v_lshl_add_u64 v[34:35], v[34:35], 0, v[142:143]
	global_store_dwordx2 v[34:35], v[30:31], off
	s_nop 0
	v_lshlrev_b32_e32 v30, 16, v32
	v_and_b32_e32 v31, 0xffff0000, v32
	v_lshlrev_b32_e32 v32, 16, v33
	v_and_b32_e32 v33, 0xffff0000, v33
	v_pk_mul_f32 v[28:29], v[28:29], v[32:33]
	v_pk_mul_f32 v[26:27], v[26:27], v[30:31]
	s_nop 0
	v_cvt_pk_bf16_f32 v26, v26, v27
	v_cvt_pk_bf16_f32 v27, v28, v29
	v_mov_b32_e32 v28, v222
	v_mov_b32_e32 v29, v223
	s_nop 0
	global_store_dwordx2 v[34:35], v[26:27], off offset:32
	s_nop 0
	v_lshlrev_b32_e32 v26, 16, v28
	v_and_b32_e32 v27, 0xffff0000, v28
	v_lshlrev_b32_e32 v28, 16, v29
	v_and_b32_e32 v29, 0xffff0000, v29
	v_pk_mul_f32 v[24:25], v[24:25], v[28:29]
	v_pk_mul_f32 v[22:23], v[22:23], v[26:27]
	v_add_u32_e32 v26, 0xb0, v144
	v_cvt_pk_bf16_f32 v22, v22, v23
	v_cvt_pk_bf16_f32 v23, v24, v25
	v_mov_b32_e32 v24, v228
	v_mov_b32_e32 v25, v229
	v_mad_i64_i32 v[28:29], s[24:25], v26, s50, v[146:147]
	global_store_dwordx2 v[34:35], v[22:23], off offset:256
	v_lshl_add_u64 v[28:29], v[28:29], 0, v[142:143]
	v_ashrrev_i32_e32 v27, 31, v26
	s_mov_b64 s[24:25], s[18:19]
	s_nop 0
	v_lshlrev_b32_e32 v22, 16, v24
	v_and_b32_e32 v23, 0xffff0000, v24
	v_lshlrev_b32_e32 v24, 16, v25
	v_and_b32_e32 v25, 0xffff0000, v25
	v_pk_mul_f32 v[16:17], v[16:17], v[24:25]
	v_pk_mul_f32 v[14:15], v[14:15], v[22:23]
	s_nop 0
	v_cvt_pk_bf16_f32 v14, v14, v15
	v_cvt_pk_bf16_f32 v15, v16, v17
	v_mov_b32_e32 v16, v230
	v_mov_b32_e32 v17, v231
	s_nop 0
	global_store_dwordx2 v[34:35], v[14:15], off offset:288
	s_nop 0
	v_lshlrev_b32_e32 v14, 16, v16
	v_and_b32_e32 v15, 0xffff0000, v16
	v_lshlrev_b32_e32 v16, 16, v17
	v_and_b32_e32 v17, 0xffff0000, v17
	v_pk_mul_f32 v[16:17], v[20:21], v[16:17]
	v_pk_mul_f32 v[14:15], v[18:19], v[14:15]
	v_lshlrev_b64 v[18:19], 12, v[26:27]
	v_cvt_pk_bf16_f32 v14, v14, v15
	v_cvt_pk_bf16_f32 v15, v16, v17
	v_mov_b32_e32 v16, v232
	v_mov_b32_e32 v17, v233
	v_lshl_add_u64 v[18:19], s[12:13], 0, v[18:19]
	v_lshl_add_u64 v[18:19], v[18:19], 0, v[142:143]
	global_store_dwordx2 v[18:19], v[14:15], off
	s_nop 0
	v_lshlrev_b32_e32 v14, 16, v16
	v_and_b32_e32 v15, 0xffff0000, v16
	v_lshlrev_b32_e32 v16, 16, v17
	v_and_b32_e32 v17, 0xffff0000, v17
	v_pk_mul_f32 v[12:13], v[12:13], v[16:17]
	v_pk_mul_f32 v[10:11], v[10:11], v[14:15]
	s_nop 0
	v_cvt_pk_bf16_f32 v10, v10, v11
	v_cvt_pk_bf16_f32 v11, v12, v13
	v_mov_b32_e32 v12, v234
	v_mov_b32_e32 v13, v235
	s_nop 0
	global_store_dwordx2 v[18:19], v[10:11], off offset:32
	s_nop 0
	v_lshlrev_b32_e32 v10, 16, v12
	v_and_b32_e32 v11, 0xffff0000, v12
	v_lshlrev_b32_e32 v12, 16, v13
	v_and_b32_e32 v13, 0xffff0000, v13
	v_pk_mul_f32 v[8:9], v[8:9], v[12:13]
	v_pk_mul_f32 v[6:7], v[6:7], v[10:11]
	s_nop 0
	v_cvt_pk_bf16_f32 v6, v6, v7
	v_cvt_pk_bf16_f32 v7, v8, v9
	v_mov_b32_e32 v8, v236
	v_mov_b32_e32 v9, v237
	s_nop 0
	global_store_dwordx2 v[18:19], v[6:7], off offset:256
	s_nop 0
	v_lshlrev_b32_e32 v6, 16, v8
	v_and_b32_e32 v7, 0xffff0000, v8
	v_lshlrev_b32_e32 v8, 16, v9
	v_and_b32_e32 v9, 0xffff0000, v9
	v_pk_mul_f32 v[2:3], v[2:3], v[6:7]
	v_pk_mul_f32 v[4:5], v[4:5], v[8:9]
	v_cvt_pk_bf16_f32 v2, v2, v3
	s_nop 0
	v_cvt_pk_bf16_f32 v3, v4, v5
	global_store_dwordx2 v[18:19], v[2:3], off offset:288
	s_cbranch_vccz .LBB0_1196
	s_waitcnt vmcnt(0)
	s_cmpk_gt_u32 s33, 0xff
	s_cbranch_scc1 .LBB0_1203
	s_barrier

.LBB0_1211:
	ds_read_b128 v[142:145], v158
	ds_read_b128 v[162:165], v158 offset:1024
	ds_read_b128 v[166:169], v158 offset:2048
	ds_read_b128 v[170:173], v158 offset:3072
	s_add_u32 s26, s24, 0xfffc0080
	s_addc_u32 s27, s25, -1
	s_cmp_eq_u32 s57, 12
	s_cselect_b32 s29, s17, s27
	s_cselect_b32 s28, s53, s26
	s_cselect_b32 s27, s15, s56
	s_cselect_b32 s26, s54, s55
	v_lshl_add_u64 v[146:147], s[24:25], 0, v[134:135]
	s_add_i32 m0, s23, 0xc000
	ds_read_b128 v[174:177], v159
	ds_read_b128 v[178:181], v159 offset:1024
	ds_read_b128 v[182:185], v159 offset:2048
	ds_read_b128 v[186:189], v159 offset:3072
	ds_read_b128 v[192:195], v159 offset:4096
	ds_read_b128 v[196:199], v159 offset:5120
	ds_read_b128 v[200:203], v159 offset:6144
	ds_read_b128 v[204:207], v159 offset:7168
	global_load_lds_dwordx4 v[146:147], off
	v_lshl_add_u64 v[146:147], s[24:25], 0, v[136:137]
	s_add_i32 m0, s23, 0xe000
	s_nop 0
	global_load_lds_dwordx4 v[146:147], off
	s_waitcnt lgkmcnt(8)
	s_barrier
	s_waitcnt lgkmcnt(0)
	s_setprio 1
	s_waitcnt lgkmcnt(0)
	v_mfma_f32_16x16x32_bf16 v[126:129], v[142:145], v[174:177], v[126:129]
	v_mfma_f32_16x16x32_bf16 v[122:125], v[166:169], v[174:177], v[122:125]
	v_mfma_f32_16x16x32_bf16 v[110:113], v[142:145], v[182:185], v[110:113]
	v_mfma_f32_16x16x32_bf16 v[106:109], v[166:169], v[182:185], v[106:109]
	v_mfma_f32_16x16x32_bf16 v[94:97], v[142:145], v[192:195], v[94:97]
	v_mfma_f32_16x16x32_bf16 v[90:93], v[166:169], v[192:195], v[90:93]
	v_mfma_f32_16x16x32_bf16 v[78:81], v[142:145], v[200:203], v[78:81]
	v_mfma_f32_16x16x32_bf16 v[74:77], v[166:169], v[200:203], v[74:77]
	v_mfma_f32_16x16x32_bf16 v[126:129], v[162:165], v[178:181], v[126:129]
	v_mfma_f32_16x16x32_bf16 v[122:125], v[170:173], v[178:181], v[122:125]
	v_mfma_f32_16x16x32_bf16 v[110:113], v[162:165], v[186:189], v[110:113]
	v_mfma_f32_16x16x32_bf16 v[106:109], v[170:173], v[186:189], v[106:109]
	v_mfma_f32_16x16x32_bf16 v[94:97], v[162:165], v[196:199], v[94:97]
	v_mfma_f32_16x16x32_bf16 v[90:93], v[170:173], v[196:199], v[90:93]
	v_mfma_f32_16x16x32_bf16 v[78:81], v[162:165], v[204:207], v[78:81]
	v_mfma_f32_16x16x32_bf16 v[74:77], v[170:173], v[204:207], v[74:77]
	s_setprio 0
	s_barrier
	s_add_i32 s58, s48, s38
	v_lshl_add_u64 v[146:147], s[26:27], 0, v[130:131]
	s_mov_b32 m0, s58
	ds_read_b128 v[208:211], v160
	ds_read_b128 v[212:215], v160 offset:1024
	ds_read_b128 v[216:219], v160 offset:2048
	ds_read_b128 v[220:223], v160 offset:3072
	global_load_lds_dwordx4 v[146:147], off
	v_lshl_add_u64 v[190:191], s[26:27], 0, v[132:133]
	s_add_i32 m0, s58, 0x2000
	s_nop 0
	global_load_lds_dwordx4 v[190:191], off
	s_barrier
	s_waitcnt lgkmcnt(0)
	s_setprio 1
	s_waitcnt lgkmcnt(0)
	v_mfma_f32_16x16x32_bf16 v[118:121], v[208:211], v[174:177], v[118:121]
	v_mfma_f32_16x16x32_bf16 v[114:117], v[216:219], v[174:177], v[114:117]
	v_mfma_f32_16x16x32_bf16 v[102:105], v[208:211], v[182:185], v[102:105]
	v_mfma_f32_16x16x32_bf16 v[98:101], v[216:219], v[182:185], v[98:101]
	v_mfma_f32_16x16x32_bf16 v[86:89], v[208:211], v[192:195], v[86:89]
	v_mfma_f32_16x16x32_bf16 v[82:85], v[216:219], v[192:195], v[82:85]
	v_mfma_f32_16x16x32_bf16 v[70:73], v[208:211], v[200:203], v[70:73]
	v_mfma_f32_16x16x32_bf16 v[66:69], v[216:219], v[200:203], v[66:69]
	v_mfma_f32_16x16x32_bf16 v[118:121], v[212:215], v[178:181], v[118:121]
	v_mfma_f32_16x16x32_bf16 v[114:117], v[220:223], v[178:181], v[114:117]
	v_mfma_f32_16x16x32_bf16 v[102:105], v[212:215], v[186:189], v[102:105]
	v_mfma_f32_16x16x32_bf16 v[98:101], v[220:223], v[186:189], v[98:101]
	v_mfma_f32_16x16x32_bf16 v[86:89], v[212:215], v[196:199], v[86:89]
	v_mfma_f32_16x16x32_bf16 v[82:85], v[220:223], v[196:199], v[82:85]
	v_mfma_f32_16x16x32_bf16 v[70:73], v[212:215], v[204:207], v[70:73]
	v_mfma_f32_16x16x32_bf16 v[66:69], v[220:223], v[204:207], v[66:69]
	s_setprio 0
	s_mov_b32 m0, s23
	v_lshl_add_u64 v[224:225], s[28:29], 0, v[130:131]
	s_barrier
	ds_read_b128 v[174:177], v159 offset:16384
	ds_read_b128 v[178:181], v159 offset:17408
	ds_read_b128 v[182:185], v159 offset:18432
	ds_read_b128 v[186:189], v159 offset:19456
	ds_read_b128 v[192:195], v159 offset:20480
	ds_read_b128 v[196:199], v159 offset:21504
	ds_read_b128 v[200:203], v159 offset:22528
	ds_read_b128 v[204:207], v159 offset:23552
	global_load_lds_dwordx4 v[224:225], off
	v_lshl_add_u64 v[226:227], s[28:29], 0, v[132:133]
	s_mov_b32 m0, s41
	s_nop 0
	global_load_lds_dwordx4 v[226:227], off
	s_barrier
	s_waitcnt lgkmcnt(0)
	s_setprio 1
	s_waitcnt lgkmcnt(0)
	v_mfma_f32_16x16x32_bf16 v[62:65], v[142:145], v[174:177], v[62:65]
	v_mfma_f32_16x16x32_bf16 v[58:61], v[166:169], v[174:177], v[58:61]
	v_mfma_f32_16x16x32_bf16 v[46:49], v[142:145], v[182:185], v[46:49]
	v_mfma_f32_16x16x32_bf16 v[42:45], v[166:169], v[182:185], v[42:45]
	v_mfma_f32_16x16x32_bf16 v[30:33], v[142:145], v[192:195], v[30:33]
	v_mfma_f32_16x16x32_bf16 v[26:29], v[166:169], v[192:195], v[26:29]
	v_mfma_f32_16x16x32_bf16 v[14:17], v[142:145], v[200:203], v[14:17]
	v_mfma_f32_16x16x32_bf16 v[10:13], v[166:169], v[200:203], v[10:13]
	v_mfma_f32_16x16x32_bf16 v[62:65], v[162:165], v[178:181], v[62:65]
	v_mfma_f32_16x16x32_bf16 v[58:61], v[170:173], v[178:181], v[58:61]
	v_mfma_f32_16x16x32_bf16 v[46:49], v[162:165], v[186:189], v[46:49]
	v_mfma_f32_16x16x32_bf16 v[42:45], v[170:173], v[186:189], v[42:45]
	v_mfma_f32_16x16x32_bf16 v[30:33], v[162:165], v[196:199], v[30:33]
	v_mfma_f32_16x16x32_bf16 v[26:29], v[170:173], v[196:199], v[26:29]
	v_mfma_f32_16x16x32_bf16 v[14:17], v[162:165], v[204:207], v[14:17]
	v_mfma_f32_16x16x32_bf16 v[10:13], v[170:173], v[204:207], v[10:13]
	s_setprio 0
	s_barrier
	s_add_u32 s58, s26, 0x40000
	s_addc_u32 s59, s27, 0
	s_add_i32 s60, s49, s38
	v_lshl_add_u64 v[142:143], s[58:59], 0, v[130:131]
	s_mov_b32 m0, s60
	s_nop 0
	global_load_lds_dwordx4 v[142:143], off
	v_lshl_add_u64 v[142:143], s[58:59], 0, v[132:133]
	s_add_i32 m0, s60, 0x2000
	s_nop 0
	global_load_lds_dwordx4 v[142:143], off
	s_waitcnt vmcnt(6)
	s_barrier
	s_setprio 1
	v_mfma_f32_16x16x32_bf16 v[54:57], v[208:211], v[174:177], v[54:57]
	v_mfma_f32_16x16x32_bf16 v[50:53], v[216:219], v[174:177], v[50:53]
	v_mfma_f32_16x16x32_bf16 v[38:41], v[208:211], v[182:185], v[38:41]
	v_mfma_f32_16x16x32_bf16 v[34:37], v[216:219], v[182:185], v[34:37]
	v_mfma_f32_16x16x32_bf16 v[22:25], v[208:211], v[192:195], v[22:25]
	v_mfma_f32_16x16x32_bf16 v[18:21], v[216:219], v[192:195], v[18:21]
	v_mfma_f32_16x16x32_bf16 v[6:9], v[208:211], v[200:203], v[6:9]
	v_mfma_f32_16x16x32_bf16 v[2:5], v[216:219], v[200:203], v[2:5]
	v_mfma_f32_16x16x32_bf16 v[54:57], v[212:215], v[178:181], v[54:57]
	v_mfma_f32_16x16x32_bf16 v[50:53], v[220:223], v[178:181], v[50:53]
	v_mfma_f32_16x16x32_bf16 v[38:41], v[212:215], v[186:189], v[38:41]
	v_mfma_f32_16x16x32_bf16 v[34:37], v[220:223], v[186:189], v[34:37]
	v_mfma_f32_16x16x32_bf16 v[22:25], v[212:215], v[196:199], v[22:25]
	v_mfma_f32_16x16x32_bf16 v[18:21], v[220:223], v[196:199], v[18:21]
	v_mfma_f32_16x16x32_bf16 v[6:9], v[212:215], v[204:207], v[6:9]
	v_mfma_f32_16x16x32_bf16 v[2:5], v[220:223], v[204:207], v[2:5]
	s_setprio 0
	s_add_i32 s58, 0, 0x18000
	v_add_u32_e32 v161, s58, v156
	s_barrier
	ds_read_b128 v[142:145], v161
	ds_read_b128 v[162:165], v161 offset:1024
	ds_read_b128 v[166:169], v161 offset:2048
	ds_read_b128 v[170:173], v161 offset:3072
	s_add_u32 s28, s28, 0x40000
	s_addc_u32 s29, s29, 0
	s_mov_b32 m0, s42
	v_lshl_add_u64 v[208:209], s[28:29], 0, v[130:131]
	ds_read_b128 v[174:177], v159 offset:32768
	ds_read_b128 v[178:181], v159 offset:33792
	ds_read_b128 v[182:185], v159 offset:34816
	ds_read_b128 v[186:189], v159 offset:35840
	ds_read_b128 v[192:195], v159 offset:36864
	ds_read_b128 v[196:199], v159 offset:37888
	ds_read_b128 v[200:203], v159 offset:38912
	ds_read_b128 v[204:207], v159 offset:39936
	global_load_lds_dwordx4 v[208:209], off
	v_lshl_add_u64 v[208:209], s[28:29], 0, v[132:133]
	s_mov_b32 m0, s43
	s_nop 0
	global_load_lds_dwordx4 v[208:209], off
	s_waitcnt lgkmcnt(8)
	s_barrier
	s_waitcnt lgkmcnt(0)
	s_setprio 1
	s_waitcnt lgkmcnt(0)
	v_mfma_f32_16x16x32_bf16 v[126:129], v[142:145], v[174:177], v[126:129]
	v_mfma_f32_16x16x32_bf16 v[122:125], v[166:169], v[174:177], v[122:125]
	v_mfma_f32_16x16x32_bf16 v[110:113], v[142:145], v[182:185], v[110:113]
	v_mfma_f32_16x16x32_bf16 v[106:109], v[166:169], v[182:185], v[106:109]
	v_mfma_f32_16x16x32_bf16 v[94:97], v[142:145], v[192:195], v[94:97]
	v_mfma_f32_16x16x32_bf16 v[90:93], v[166:169], v[192:195], v[90:93]
	v_mfma_f32_16x16x32_bf16 v[78:81], v[142:145], v[200:203], v[78:81]
	v_mfma_f32_16x16x32_bf16 v[74:77], v[166:169], v[200:203], v[74:77]
	v_mfma_f32_16x16x32_bf16 v[126:129], v[162:165], v[178:181], v[126:129]
	v_mfma_f32_16x16x32_bf16 v[122:125], v[170:173], v[178:181], v[122:125]
	v_mfma_f32_16x16x32_bf16 v[110:113], v[162:165], v[186:189], v[110:113]
	v_mfma_f32_16x16x32_bf16 v[106:109], v[170:173], v[186:189], v[106:109]
	v_mfma_f32_16x16x32_bf16 v[94:97], v[162:165], v[196:199], v[94:97]
	v_mfma_f32_16x16x32_bf16 v[90:93], v[170:173], v[196:199], v[90:93]
	v_mfma_f32_16x16x32_bf16 v[78:81], v[162:165], v[204:207], v[78:81]
	v_mfma_f32_16x16x32_bf16 v[74:77], v[170:173], v[204:207], v[74:77]
	s_setprio 0
	s_barrier
	s_add_i32 s28, 0, 0x1c000
	s_add_i32 s29, s58, s38
	v_add_u32_e32 v161, s28, v156
	v_lshl_add_u64 v[146:147], v[146:147], 0, s[8:9]
	s_mov_b32 m0, s29
	ds_read_b128 v[208:211], v161
	ds_read_b128 v[212:215], v161 offset:1024
	ds_read_b128 v[216:219], v161 offset:2048
	ds_read_b128 v[220:223], v161 offset:3072
	global_load_lds_dwordx4 v[146:147], off
	v_lshl_add_u64 v[146:147], v[190:191], 0, s[8:9]
	s_add_i32 m0, s29, 0x2000
	s_nop 0
	global_load_lds_dwordx4 v[146:147], off
	s_barrier
	s_waitcnt lgkmcnt(0)
	s_setprio 1
	s_waitcnt lgkmcnt(0)
	v_mfma_f32_16x16x32_bf16 v[118:121], v[208:211], v[174:177], v[118:121]
	v_mfma_f32_16x16x32_bf16 v[114:117], v[216:219], v[174:177], v[114:117]
	v_mfma_f32_16x16x32_bf16 v[102:105], v[208:211], v[182:185], v[102:105]
	v_mfma_f32_16x16x32_bf16 v[98:101], v[216:219], v[182:185], v[98:101]
	v_mfma_f32_16x16x32_bf16 v[86:89], v[208:211], v[192:195], v[86:89]
	v_mfma_f32_16x16x32_bf16 v[82:85], v[216:219], v[192:195], v[82:85]
	v_mfma_f32_16x16x32_bf16 v[70:73], v[208:211], v[200:203], v[70:73]
	v_mfma_f32_16x16x32_bf16 v[66:69], v[216:219], v[200:203], v[66:69]
	v_mfma_f32_16x16x32_bf16 v[118:121], v[212:215], v[178:181], v[118:121]
	v_mfma_f32_16x16x32_bf16 v[114:117], v[220:223], v[178:181], v[114:117]
	v_mfma_f32_16x16x32_bf16 v[102:105], v[212:215], v[186:189], v[102:105]
	v_mfma_f32_16x16x32_bf16 v[98:101], v[220:223], v[186:189], v[98:101]
	v_mfma_f32_16x16x32_bf16 v[86:89], v[212:215], v[196:199], v[86:89]
	v_mfma_f32_16x16x32_bf16 v[82:85], v[220:223], v[196:199], v[82:85]
	v_mfma_f32_16x16x32_bf16 v[70:73], v[212:215], v[204:207], v[70:73]
	v_mfma_f32_16x16x32_bf16 v[66:69], v[220:223], v[204:207], v[66:69]
	s_setprio 0
	s_mov_b32 m0, s45
	v_lshl_add_u64 v[146:147], v[224:225], 0, s[8:9]
	s_barrier
	ds_read_b128 v[174:177], v159 offset:49152
	ds_read_b128 v[178:181], v159 offset:50176
	ds_read_b128 v[182:185], v159 offset:51200
	ds_read_b128 v[186:189], v159 offset:52224
	ds_read_b128 v[192:195], v159 offset:53248
	ds_read_b128 v[196:199], v159 offset:54272
	ds_read_b128 v[200:203], v159 offset:55296
	ds_read_b128 v[204:207], v159 offset:56320
	global_load_lds_dwordx4 v[146:147], off
	v_lshl_add_u64 v[146:147], v[226:227], 0, s[8:9]
	s_mov_b32 m0, s46
	s_nop 0
	global_load_lds_dwordx4 v[146:147], off
	s_barrier
	s_waitcnt lgkmcnt(0)
	s_setprio 1
	s_waitcnt lgkmcnt(0)
	v_mfma_f32_16x16x32_bf16 v[62:65], v[142:145], v[174:177], v[62:65]
	v_mfma_f32_16x16x32_bf16 v[58:61], v[166:169], v[174:177], v[58:61]
	v_mfma_f32_16x16x32_bf16 v[46:49], v[142:145], v[182:185], v[46:49]
	v_mfma_f32_16x16x32_bf16 v[42:45], v[166:169], v[182:185], v[42:45]
	v_mfma_f32_16x16x32_bf16 v[30:33], v[142:145], v[192:195], v[30:33]
	v_mfma_f32_16x16x32_bf16 v[26:29], v[166:169], v[192:195], v[26:29]
	v_mfma_f32_16x16x32_bf16 v[14:17], v[142:145], v[200:203], v[14:17]
	v_mfma_f32_16x16x32_bf16 v[10:13], v[166:169], v[200:203], v[10:13]
	v_mfma_f32_16x16x32_bf16 v[62:65], v[162:165], v[178:181], v[62:65]
	v_mfma_f32_16x16x32_bf16 v[58:61], v[170:173], v[178:181], v[58:61]
	v_mfma_f32_16x16x32_bf16 v[46:49], v[162:165], v[186:189], v[46:49]
	v_mfma_f32_16x16x32_bf16 v[42:45], v[170:173], v[186:189], v[42:45]
	v_mfma_f32_16x16x32_bf16 v[30:33], v[162:165], v[196:199], v[30:33]
	v_mfma_f32_16x16x32_bf16 v[26:29], v[170:173], v[196:199], v[26:29]
	v_mfma_f32_16x16x32_bf16 v[14:17], v[162:165], v[204:207], v[14:17]
	v_mfma_f32_16x16x32_bf16 v[10:13], v[170:173], v[204:207], v[10:13]
	s_setprio 0
	s_barrier
	s_add_u32 s26, s26, 0x40080
	s_addc_u32 s27, s27, 0
	s_add_i32 s28, s28, s38
	v_lshl_add_u64 v[142:143], s[26:27], 0, v[130:131]
	s_mov_b32 m0, s28
	s_nop 0
	global_load_lds_dwordx4 v[142:143], off
	v_lshl_add_u64 v[142:143], s[26:27], 0, v[132:133]
	s_add_i32 m0, s28, 0x2000
	s_nop 0
	global_load_lds_dwordx4 v[142:143], off
	s_waitcnt vmcnt(6)
	s_barrier
	s_setprio 1
	v_mfma_f32_16x16x32_bf16 v[54:57], v[208:211], v[174:177], v[54:57]
	v_mfma_f32_16x16x32_bf16 v[50:53], v[216:219], v[174:177], v[50:53]
	v_mfma_f32_16x16x32_bf16 v[38:41], v[208:211], v[182:185], v[38:41]
	v_mfma_f32_16x16x32_bf16 v[34:37], v[216:219], v[182:185], v[34:37]
	v_mfma_f32_16x16x32_bf16 v[22:25], v[208:211], v[192:195], v[22:25]
	v_mfma_f32_16x16x32_bf16 v[18:21], v[216:219], v[192:195], v[18:21]
	v_mfma_f32_16x16x32_bf16 v[6:9], v[208:211], v[200:203], v[6:9]
	v_mfma_f32_16x16x32_bf16 v[2:5], v[216:219], v[200:203], v[2:5]
	v_mfma_f32_16x16x32_bf16 v[54:57], v[212:215], v[178:181], v[54:57]
	v_mfma_f32_16x16x32_bf16 v[50:53], v[220:223], v[178:181], v[50:53]
	v_mfma_f32_16x16x32_bf16 v[38:41], v[212:215], v[186:189], v[38:41]
	v_mfma_f32_16x16x32_bf16 v[34:37], v[220:223], v[186:189], v[34:37]
	v_mfma_f32_16x16x32_bf16 v[22:25], v[212:215], v[196:199], v[22:25]
	v_mfma_f32_16x16x32_bf16 v[18:21], v[220:223], v[196:199], v[18:21]
	v_mfma_f32_16x16x32_bf16 v[6:9], v[212:215], v[204:207], v[6:9]
	v_mfma_f32_16x16x32_bf16 v[2:5], v[220:223], v[204:207], v[2:5]
	s_setprio 0
	s_add_i32 s57, s57, 2
	s_add_u32 s24, s24, 0x100
	s_addc_u32 s25, s25, 0
	s_add_u32 s55, s55, 0x100
	s_addc_u32 s56, s56, 0
	s_cmp_gt_u32 s57, 13
	s_barrier
	s_cbranch_scc0 .LBB0_1211
	v_lshl_or_b32 v142, s52, 8, v157
	v_lshl_add_u32 v144, s22, 8, v155
	v_ashrrev_i32_e32 v143, 31, v142
	v_mov_b64_e32 v[146:147], s[6:7]
	v_ashrrev_i32_e32 v145, 31, v144
	v_mad_i64_i32 v[162:163], s[24:25], v144, s50, v[146:147]
	v_lshlrev_b64 v[142:143], 1, v[142:143]
	v_lshl_add_u64 v[162:163], v[162:163], 0, v[142:143]
	v_lshlrev_b64 v[166:167], 12, v[144:145]
	v_add_co_u32_e32 v164, vcc, 0x2ec41000, v162
	v_lshl_add_u64 v[166:167], s[10:11], 0, v[166:167]
	s_nop 0
	v_addc_co_u32_e32 v165, vcc, 0, v163, vcc
	v_lshl_add_u64 v[166:167], v[166:167], 0, v[142:143]
	v_mov_b32_e32 v228, v164
	v_mov_b32_e32 v229, v165
	v_mov_b32_e32 v232, v166
	v_mov_b32_e32 v233, v167
	v_mov_b32_e32 v237, 0x1000
	global_load_dwordx2 v[174:175], v[228:229], off
	global_load_dwordx2 v[176:177], v[232:233], off
	global_load_dwordx2 v[178:179], v[228:229], off offset:32
	global_load_dwordx2 v[180:181], v[232:233], off offset:32
	global_load_dwordx2 v[182:183], v[228:229], off offset:256
	global_load_dwordx2 v[184:185], v[232:233], off offset:256
	global_load_dwordx2 v[186:187], v[228:229], off offset:288
	global_load_dwordx2 v[188:189], v[232:233], off offset:288
	v_mov_b32_e32 v236, 16
	v_mad_i64_i32 v[230:231], s[24:25], v236, s50, v[228:229]
	v_mad_i64_i32 v[234:235], s[24:25], v236, v237, v[232:233]
	global_load_dwordx2 v[192:193], v[230:231], off
	global_load_dwordx2 v[194:195], v[234:235], off
	global_load_dwordx2 v[196:197], v[230:231], off offset:32
	global_load_dwordx2 v[198:199], v[234:235], off offset:32
	global_load_dwordx2 v[200:201], v[230:231], off offset:256
	global_load_dwordx2 v[202:203], v[234:235], off offset:256
	global_load_dwordx2 v[204:205], v[230:231], off offset:288
	global_load_dwordx2 v[206:207], v[234:235], off offset:288
	v_mov_b32_e32 v236, 32
	v_mad_i64_i32 v[230:231], s[24:25], v236, s50, v[228:229]
	v_mad_i64_i32 v[234:235], s[24:25], v236, v237, v[232:233]
	global_load_dwordx2 v[208:209], v[230:231], off
	global_load_dwordx2 v[210:211], v[234:235], off
	global_load_dwordx2 v[212:213], v[230:231], off offset:32
	global_load_dwordx2 v[214:215], v[234:235], off offset:32
	global_load_dwordx2 v[216:217], v[230:231], off offset:256
	global_load_dwordx2 v[218:219], v[234:235], off offset:256
	global_load_dwordx2 v[220:221], v[230:231], off offset:288
	global_load_dwordx2 v[222:223], v[234:235], off offset:288
	s_waitcnt vmcnt(0)
	v_mov_b32_e32 v164, v174
	v_mov_b32_e32 v165, v175
	v_lshl_add_u64 v[162:163], v[162:163], 0, s[12:13]
	v_mov_b32_e32 v168, v176
	v_mov_b32_e32 v169, v177
	s_mov_b32 s52, s14
	s_mov_b32 s22, s16
	s_mov_b64 s[26:27], s[20:21]
	s_nop 0
	v_lshlrev_b32_e32 v170, 16, v164
	v_and_b32_e32 v171, 0xffff0000, v164
	v_lshlrev_b32_e32 v164, 16, v165
	v_and_b32_e32 v165, 0xffff0000, v165
	v_lshlrev_b32_e32 v172, 16, v168
	v_and_b32_e32 v173, 0xffff0000, v168
	v_lshlrev_b32_e32 v168, 16, v169
	v_and_b32_e32 v169, 0xffff0000, v169
	v_pk_fma_f32 v[128:129], v[128:129], v[164:165], v[168:169]
	v_pk_fma_f32 v[126:127], v[126:127], v[170:171], v[172:173]
	s_nop 0
	v_cvt_pk_bf16_f32 v126, v126, v127
	v_cvt_pk_bf16_f32 v127, v128, v129
	v_mov_b32_e32 v128, v178
	v_mov_b32_e32 v129, v179
	v_mov_b32_e32 v164, v180
	v_mov_b32_e32 v165, v181
	s_nop 0
	v_lshlrev_b32_e32 v168, 16, v164
	global_store_dwordx2 v[166:167], v[126:127], off
	v_lshlrev_b32_e32 v126, 16, v128
	v_and_b32_e32 v127, 0xffff0000, v128
	v_lshlrev_b32_e32 v128, 16, v129
	v_and_b32_e32 v129, 0xffff0000, v129
	v_and_b32_e32 v169, 0xffff0000, v164
	v_lshlrev_b32_e32 v164, 16, v165
	v_and_b32_e32 v165, 0xffff0000, v165
	v_pk_fma_f32 v[124:125], v[124:125], v[128:129], v[164:165]
	v_pk_fma_f32 v[122:123], v[122:123], v[126:127], v[168:169]
	s_nop 0
	v_cvt_pk_bf16_f32 v122, v122, v123
	v_cvt_pk_bf16_f32 v123, v124, v125
	v_mov_b32_e32 v124, v182
	v_mov_b32_e32 v125, v183
	v_mov_b32_e32 v126, v184
	v_mov_b32_e32 v127, v185
	s_nop 0
	v_lshlrev_b32_e32 v128, 16, v126
	global_store_dwordx2 v[166:167], v[122:123], off offset:32
	v_lshlrev_b32_e32 v122, 16, v124
	v_and_b32_e32 v123, 0xffff0000, v124
	v_lshlrev_b32_e32 v124, 16, v125
	v_and_b32_e32 v125, 0xffff0000, v125
	v_and_b32_e32 v129, 0xffff0000, v126
	v_lshlrev_b32_e32 v126, 16, v127
	v_and_b32_e32 v127, 0xffff0000, v127
	v_pk_fma_f32 v[120:121], v[120:121], v[124:125], v[126:127]
	v_pk_fma_f32 v[118:119], v[118:119], v[122:123], v[128:129]
	v_or_b32_e32 v124, 16, v144
	v_cvt_pk_bf16_f32 v118, v118, v119
	v_cvt_pk_bf16_f32 v119, v120, v121
	v_mov_b32_e32 v120, v186
	v_mov_b32_e32 v121, v187
	v_mov_b32_e32 v122, v188
	v_mov_b32_e32 v123, v189
	v_ashrrev_i32_e32 v125, 31, v124
	v_mad_i64_i32 v[126:127], s[24:25], v124, s50, v[146:147]
	global_store_dwordx2 v[166:167], v[118:119], off offset:256
	v_lshl_add_u64 v[126:127], v[126:127], 0, v[142:143]
	v_add_co_u32_e32 v128, vcc, s51, v126
	s_nop 0
	v_lshlrev_b32_e32 v118, 16, v120
	v_and_b32_e32 v119, 0xffff0000, v120
	v_lshlrev_b32_e32 v162, 16, v122
	v_and_b32_e32 v163, 0xffff0000, v122
	v_pk_fma_f32 v[114:115], v[114:115], v[118:119], v[162:163]
	v_lshlrev_b64 v[118:119], 12, v[124:125]
	v_lshlrev_b32_e32 v120, 16, v121
	v_and_b32_e32 v121, 0xffff0000, v121
	v_lshlrev_b32_e32 v122, 16, v123
	v_and_b32_e32 v123, 0xffff0000, v123
	v_lshl_add_u64 v[118:119], s[10:11], 0, v[118:119]
	v_addc_co_u32_e32 v129, vcc, 0, v127, vcc
	v_pk_fma_f32 v[116:117], v[116:117], v[120:121], v[122:123]
	v_lshl_add_u64 v[118:119], v[118:119], 0, v[142:143]
	v_cvt_pk_bf16_f32 v114, v114, v115
	v_cvt_pk_bf16_f32 v115, v116, v117
	v_mov_b32_e32 v116, v192
	v_mov_b32_e32 v117, v193
	v_mov_b32_e32 v120, v194
	v_mov_b32_e32 v121, v195
	v_lshl_add_u64 v[122:123], v[126:127], 0, s[12:13]
	global_store_dwordx2 v[166:167], v[114:115], off offset:288
	s_nop 0
	v_lshlrev_b32_e32 v114, 16, v116
	v_and_b32_e32 v115, 0xffff0000, v116
	v_lshlrev_b32_e32 v116, 16, v117
	v_and_b32_e32 v117, 0xffff0000, v117
	v_lshlrev_b32_e32 v124, 16, v120
	v_and_b32_e32 v125, 0xffff0000, v120
	v_lshlrev_b32_e32 v120, 16, v121
	v_and_b32_e32 v121, 0xffff0000, v121
	v_pk_fma_f32 v[112:113], v[112:113], v[116:117], v[120:121]
	v_pk_fma_f32 v[110:111], v[110:111], v[114:115], v[124:125]
	s_nop 0
	v_cvt_pk_bf16_f32 v110, v110, v111
	v_cvt_pk_bf16_f32 v111, v112, v113
	v_mov_b32_e32 v112, v196
	v_mov_b32_e32 v113, v197
	v_mov_b32_e32 v114, v198
	v_mov_b32_e32 v115, v199
	s_nop 0
	v_lshlrev_b32_e32 v116, 16, v114
	global_store_dwordx2 v[118:119], v[110:111], off
	v_lshlrev_b32_e32 v110, 16, v112
	v_and_b32_e32 v111, 0xffff0000, v112
	v_lshlrev_b32_e32 v112, 16, v113
	v_and_b32_e32 v113, 0xffff0000, v113
	v_and_b32_e32 v117, 0xffff0000, v114
	v_lshlrev_b32_e32 v114, 16, v115
	v_and_b32_e32 v115, 0xffff0000, v115
	v_pk_fma_f32 v[108:109], v[108:109], v[112:113], v[114:115]
	v_pk_fma_f32 v[106:107], v[106:107], v[110:111], v[116:117]
	s_nop 0
	v_cvt_pk_bf16_f32 v106, v106, v107
	v_cvt_pk_bf16_f32 v107, v108, v109
	v_mov_b32_e32 v108, v200
	v_mov_b32_e32 v109, v201
	v_mov_b32_e32 v110, v202
	v_mov_b32_e32 v111, v203
	s_nop 0
	v_lshlrev_b32_e32 v112, 16, v110
	global_store_dwordx2 v[118:119], v[106:107], off offset:32
	v_lshlrev_b32_e32 v106, 16, v108
	v_and_b32_e32 v107, 0xffff0000, v108
	v_lshlrev_b32_e32 v108, 16, v109
	v_and_b32_e32 v109, 0xffff0000, v109
	v_and_b32_e32 v113, 0xffff0000, v110
	v_lshlrev_b32_e32 v110, 16, v111
	v_and_b32_e32 v111, 0xffff0000, v111
	v_pk_fma_f32 v[104:105], v[104:105], v[108:109], v[110:111]
	v_pk_fma_f32 v[102:103], v[102:103], v[106:107], v[112:113]
	v_or_b32_e32 v108, 32, v144
	v_cvt_pk_bf16_f32 v102, v102, v103
	v_cvt_pk_bf16_f32 v103, v104, v105
	v_mov_b32_e32 v104, v204
	v_mov_b32_e32 v105, v205
	v_mov_b32_e32 v106, v206
	v_mov_b32_e32 v107, v207
	v_ashrrev_i32_e32 v109, 31, v108
	v_mad_i64_i32 v[110:111], s[24:25], v108, s50, v[146:147]
	global_store_dwordx2 v[118:119], v[102:103], off offset:256
	v_lshl_add_u64 v[110:111], v[110:111], 0, v[142:143]
	v_add_co_u32_e32 v112, vcc, s51, v110
	s_nop 0
	v_lshlrev_b32_e32 v102, 16, v104
	v_and_b32_e32 v103, 0xffff0000, v104
	v_lshlrev_b32_e32 v114, 16, v106
	v_and_b32_e32 v115, 0xffff0000, v106
	v_pk_fma_f32 v[98:99], v[98:99], v[102:103], v[114:115]
	v_lshlrev_b64 v[102:103], 12, v[108:109]
	v_lshlrev_b32_e32 v104, 16, v105
	v_and_b32_e32 v105, 0xffff0000, v105
	v_lshlrev_b32_e32 v106, 16, v107
	v_and_b32_e32 v107, 0xffff0000, v107
	v_lshl_add_u64 v[102:103], s[10:11], 0, v[102:103]
	v_addc_co_u32_e32 v113, vcc, 0, v111, vcc
	v_pk_fma_f32 v[100:101], v[100:101], v[104:105], v[106:107]
	v_lshl_add_u64 v[102:103], v[102:103], 0, v[142:143]
	v_cvt_pk_bf16_f32 v98, v98, v99
	v_cvt_pk_bf16_f32 v99, v100, v101
	v_mov_b32_e32 v100, v208
	v_mov_b32_e32 v101, v209
	v_mov_b32_e32 v104, v210
	v_mov_b32_e32 v105, v211
	v_lshl_add_u64 v[106:107], v[110:111], 0, s[12:13]
	global_store_dwordx2 v[118:119], v[98:99], off offset:288
	s_nop 0
	v_lshlrev_b32_e32 v98, 16, v100
	v_and_b32_e32 v99, 0xffff0000, v100
	v_lshlrev_b32_e32 v100, 16, v101
	v_and_b32_e32 v101, 0xffff0000, v101
	v_lshlrev_b32_e32 v108, 16, v104
	v_and_b32_e32 v109, 0xffff0000, v104
	v_lshlrev_b32_e32 v104, 16, v105
	v_and_b32_e32 v105, 0xffff0000, v105
	v_pk_fma_f32 v[96:97], v[96:97], v[100:101], v[104:105]
	v_pk_fma_f32 v[94:95], v[94:95], v[98:99], v[108:109]
	s_nop 0
	v_cvt_pk_bf16_f32 v94, v94, v95
	v_cvt_pk_bf16_f32 v95, v96, v97
	v_mov_b32_e32 v96, v212
	v_mov_b32_e32 v97, v213
	v_mov_b32_e32 v98, v214
	v_mov_b32_e32 v99, v215
	s_nop 0
	v_lshlrev_b32_e32 v100, 16, v98
	global_store_dwordx2 v[102:103], v[94:95], off
	v_lshlrev_b32_e32 v94, 16, v96
	v_and_b32_e32 v95, 0xffff0000, v96
	v_lshlrev_b32_e32 v96, 16, v97
	v_and_b32_e32 v97, 0xffff0000, v97
	v_and_b32_e32 v101, 0xffff0000, v98
	v_lshlrev_b32_e32 v98, 16, v99
	v_and_b32_e32 v99, 0xffff0000, v99
	v_pk_fma_f32 v[92:93], v[92:93], v[96:97], v[98:99]
	v_pk_fma_f32 v[90:91], v[90:91], v[94:95], v[100:101]
	s_nop 0
	v_cvt_pk_bf16_f32 v90, v90, v91
	v_cvt_pk_bf16_f32 v91, v92, v93
	v_mov_b32_e32 v92, v216
	v_mov_b32_e32 v93, v217
	v_mov_b32_e32 v94, v218
	v_mov_b32_e32 v95, v219
	s_nop 0
	v_lshlrev_b32_e32 v96, 16, v94
	global_store_dwordx2 v[102:103], v[90:91], off offset:32
	v_lshlrev_b32_e32 v90, 16, v92
	v_and_b32_e32 v91, 0xffff0000, v92
	v_lshlrev_b32_e32 v92, 16, v93
	v_and_b32_e32 v93, 0xffff0000, v93
	v_and_b32_e32 v97, 0xffff0000, v94
	v_lshlrev_b32_e32 v94, 16, v95
	v_and_b32_e32 v95, 0xffff0000, v95
	v_pk_fma_f32 v[88:89], v[88:89], v[92:93], v[94:95]
	v_pk_fma_f32 v[86:87], v[86:87], v[90:91], v[96:97]
	v_or_b32_e32 v92, 48, v144
	v_cvt_pk_bf16_f32 v86, v86, v87
	v_cvt_pk_bf16_f32 v87, v88, v89
	v_mov_b32_e32 v88, v220
	v_mov_b32_e32 v89, v221
	v_mov_b32_e32 v90, v222
	v_mov_b32_e32 v91, v223
	v_ashrrev_i32_e32 v93, 31, v92
	v_mad_i64_i32 v[94:95], s[24:25], v92, s50, v[146:147]
	global_store_dwordx2 v[102:103], v[86:87], off offset:256
	v_lshl_add_u64 v[94:95], v[94:95], 0, v[142:143]
	v_add_co_u32_e32 v96, vcc, s51, v94
	s_nop 0
	v_lshlrev_b32_e32 v86, 16, v88
	v_and_b32_e32 v87, 0xffff0000, v88
	v_lshlrev_b32_e32 v98, 16, v90
	v_and_b32_e32 v99, 0xffff0000, v90
	v_pk_fma_f32 v[82:83], v[82:83], v[86:87], v[98:99]
	v_lshlrev_b64 v[86:87], 12, v[92:93]
	v_lshlrev_b32_e32 v88, 16, v89
	v_and_b32_e32 v89, 0xffff0000, v89
	v_lshlrev_b32_e32 v90, 16, v91
	v_and_b32_e32 v91, 0xffff0000, v91
	v_lshl_add_u64 v[86:87], s[10:11], 0, v[86:87]
	v_addc_co_u32_e32 v97, vcc, 0, v95, vcc
	v_pk_fma_f32 v[84:85], v[84:85], v[88:89], v[90:91]
	v_lshl_add_u64 v[86:87], v[86:87], 0, v[142:143]
	v_cvt_pk_bf16_f32 v82, v82, v83
	v_cvt_pk_bf16_f32 v83, v84, v85
	v_mov_b32_e32 v237, 0x1000
	v_mov_b32_e32 v236, 48
	v_mad_i64_i32 v[230:231], s[24:25], v236, s50, v[228:229]
	v_mad_i64_i32 v[234:235], s[24:25], v236, v237, v[232:233]
	global_load_dwordx2 v[174:175], v[230:231], off
	global_load_dwordx2 v[176:177], v[234:235], off
	global_load_dwordx2 v[178:179], v[230:231], off offset:32
	global_load_dwordx2 v[180:181], v[234:235], off offset:32
	global_load_dwordx2 v[182:183], v[230:231], off offset:256
	global_load_dwordx2 v[184:185], v[234:235], off offset:256
	global_load_dwordx2 v[186:187], v[230:231], off offset:288
	global_load_dwordx2 v[188:189], v[234:235], off offset:288
	v_mov_b32_e32 v236, 128
	v_mad_i64_i32 v[230:231], s[24:25], v236, s50, v[228:229]
	v_mad_i64_i32 v[234:235], s[24:25], v236, v237, v[232:233]
	global_load_dwordx2 v[192:193], v[230:231], off
	global_load_dwordx2 v[194:195], v[234:235], off
	global_load_dwordx2 v[196:197], v[230:231], off offset:32
	global_load_dwordx2 v[198:199], v[234:235], off offset:32
	global_load_dwordx2 v[200:201], v[230:231], off offset:256
	global_load_dwordx2 v[202:203], v[234:235], off offset:256
	global_load_dwordx2 v[204:205], v[230:231], off offset:288
	global_load_dwordx2 v[206:207], v[234:235], off offset:288
	v_mov_b32_e32 v236, 144
	v_mad_i64_i32 v[230:231], s[24:25], v236, s50, v[228:229]
	v_mad_i64_i32 v[234:235], s[24:25], v236, v237, v[232:233]
	global_load_dwordx2 v[208:209], v[230:231], off
	global_load_dwordx2 v[210:211], v[234:235], off
	global_load_dwordx2 v[212:213], v[230:231], off offset:32
	global_load_dwordx2 v[214:215], v[234:235], off offset:32
	global_load_dwordx2 v[216:217], v[230:231], off offset:256
	global_load_dwordx2 v[218:219], v[234:235], off offset:256
	global_load_dwordx2 v[220:221], v[230:231], off offset:288
	global_load_dwordx2 v[222:223], v[234:235], off offset:288
	s_waitcnt vmcnt(0)
	v_mov_b32_e32 v84, v174
	v_mov_b32_e32 v85, v175
	v_mov_b32_e32 v88, v176
	v_mov_b32_e32 v89, v177
	v_lshl_add_u64 v[90:91], v[94:95], 0, s[12:13]
	global_store_dwordx2 v[102:103], v[82:83], off offset:288
	s_nop 0
	v_lshlrev_b32_e32 v82, 16, v84
	v_and_b32_e32 v83, 0xffff0000, v84
	v_lshlrev_b32_e32 v84, 16, v85
	v_and_b32_e32 v85, 0xffff0000, v85
	v_lshlrev_b32_e32 v92, 16, v88
	v_and_b32_e32 v93, 0xffff0000, v88
	v_lshlrev_b32_e32 v88, 16, v89
	v_and_b32_e32 v89, 0xffff0000, v89
	v_pk_fma_f32 v[80:81], v[80:81], v[84:85], v[88:89]
	v_pk_fma_f32 v[78:79], v[78:79], v[82:83], v[92:93]
	s_nop 0
	v_cvt_pk_bf16_f32 v78, v78, v79
	v_cvt_pk_bf16_f32 v79, v80, v81
	v_mov_b32_e32 v80, v178
	v_mov_b32_e32 v81, v179
	v_mov_b32_e32 v82, v180
	v_mov_b32_e32 v83, v181
	s_nop 0
	v_lshlrev_b32_e32 v84, 16, v82
	global_store_dwordx2 v[86:87], v[78:79], off
	v_lshlrev_b32_e32 v78, 16, v80
	v_and_b32_e32 v79, 0xffff0000, v80
	v_lshlrev_b32_e32 v80, 16, v81
	v_and_b32_e32 v81, 0xffff0000, v81
	v_and_b32_e32 v85, 0xffff0000, v82
	v_lshlrev_b32_e32 v82, 16, v83
	v_and_b32_e32 v83, 0xffff0000, v83
	v_pk_fma_f32 v[76:77], v[76:77], v[80:81], v[82:83]
	v_pk_fma_f32 v[74:75], v[74:75], v[78:79], v[84:85]
	s_nop 0
	v_cvt_pk_bf16_f32 v74, v74, v75
	v_cvt_pk_bf16_f32 v75, v76, v77
	v_mov_b32_e32 v76, v182
	v_mov_b32_e32 v77, v183
	v_mov_b32_e32 v78, v184
	v_mov_b32_e32 v79, v185
	s_nop 0
	v_lshlrev_b32_e32 v80, 16, v78
	global_store_dwordx2 v[86:87], v[74:75], off offset:32
	v_lshlrev_b32_e32 v74, 16, v76
	v_and_b32_e32 v75, 0xffff0000, v76
	v_lshlrev_b32_e32 v76, 16, v77
	v_and_b32_e32 v77, 0xffff0000, v77
	v_and_b32_e32 v81, 0xffff0000, v78
	v_lshlrev_b32_e32 v78, 16, v79
	v_and_b32_e32 v79, 0xffff0000, v79
	v_pk_fma_f32 v[72:73], v[72:73], v[76:77], v[78:79]
	v_pk_fma_f32 v[70:71], v[70:71], v[74:75], v[80:81]
	v_add_u32_e32 v76, 0x80, v144
	v_cvt_pk_bf16_f32 v70, v70, v71
	v_cvt_pk_bf16_f32 v71, v72, v73
	v_mov_b32_e32 v72, v186
	v_mov_b32_e32 v73, v187
	v_mov_b32_e32 v74, v188
	v_mov_b32_e32 v75, v189
	v_ashrrev_i32_e32 v77, 31, v76
	v_mad_i64_i32 v[78:79], s[24:25], v76, s50, v[146:147]
	global_store_dwordx2 v[86:87], v[70:71], off offset:256
	v_lshl_add_u64 v[78:79], v[78:79], 0, v[142:143]
	v_add_co_u32_e32 v80, vcc, s51, v78
	s_nop 0
	v_lshlrev_b32_e32 v70, 16, v72
	v_and_b32_e32 v71, 0xffff0000, v72
	v_lshlrev_b32_e32 v82, 16, v74
	v_and_b32_e32 v83, 0xffff0000, v74
	v_pk_fma_f32 v[66:67], v[66:67], v[70:71], v[82:83]
	v_lshlrev_b64 v[70:71], 12, v[76:77]
	v_lshlrev_b32_e32 v72, 16, v73
	v_and_b32_e32 v73, 0xffff0000, v73
	v_lshlrev_b32_e32 v74, 16, v75
	v_and_b32_e32 v75, 0xffff0000, v75
	v_lshl_add_u64 v[70:71], s[10:11], 0, v[70:71]
	v_addc_co_u32_e32 v81, vcc, 0, v79, vcc
	v_pk_fma_f32 v[68:69], v[68:69], v[72:73], v[74:75]
	v_lshl_add_u64 v[70:71], v[70:71], 0, v[142:143]
	v_cvt_pk_bf16_f32 v66, v66, v67
	v_cvt_pk_bf16_f32 v67, v68, v69
	v_mov_b32_e32 v68, v192
	v_mov_b32_e32 v69, v193
	v_mov_b32_e32 v72, v194
	v_mov_b32_e32 v73, v195
	v_lshl_add_u64 v[74:75], v[78:79], 0, s[12:13]
	global_store_dwordx2 v[86:87], v[66:67], off offset:288
	s_nop 0
	v_lshlrev_b32_e32 v66, 16, v68
	v_and_b32_e32 v67, 0xffff0000, v68
	v_lshlrev_b32_e32 v68, 16, v69
	v_and_b32_e32 v69, 0xffff0000, v69
	v_lshlrev_b32_e32 v76, 16, v72
	v_and_b32_e32 v77, 0xffff0000, v72
	v_lshlrev_b32_e32 v72, 16, v73
	v_and_b32_e32 v73, 0xffff0000, v73
	v_pk_fma_f32 v[64:65], v[64:65], v[68:69], v[72:73]
	v_pk_fma_f32 v[62:63], v[62:63], v[66:67], v[76:77]
	s_nop 0
	v_cvt_pk_bf16_f32 v62, v62, v63
	v_cvt_pk_bf16_f32 v63, v64, v65
	v_mov_b32_e32 v64, v196
	v_mov_b32_e32 v65, v197
	v_mov_b32_e32 v66, v198
	v_mov_b32_e32 v67, v199
	s_nop 0
	v_lshlrev_b32_e32 v68, 16, v66
	global_store_dwordx2 v[70:71], v[62:63], off
	v_lshlrev_b32_e32 v62, 16, v64
	v_and_b32_e32 v63, 0xffff0000, v64
	v_lshlrev_b32_e32 v64, 16, v65
	v_and_b32_e32 v65, 0xffff0000, v65
	v_and_b32_e32 v69, 0xffff0000, v66
	v_lshlrev_b32_e32 v66, 16, v67
	v_and_b32_e32 v67, 0xffff0000, v67
	v_pk_fma_f32 v[60:61], v[60:61], v[64:65], v[66:67]
	v_pk_fma_f32 v[58:59], v[58:59], v[62:63], v[68:69]
	s_nop 0
	v_cvt_pk_bf16_f32 v58, v58, v59
	v_cvt_pk_bf16_f32 v59, v60, v61
	v_mov_b32_e32 v60, v200
	v_mov_b32_e32 v61, v201
	v_mov_b32_e32 v62, v202
	v_mov_b32_e32 v63, v203
	s_nop 0
	v_lshlrev_b32_e32 v64, 16, v62
	global_store_dwordx2 v[70:71], v[58:59], off offset:32
	v_lshlrev_b32_e32 v58, 16, v60
	v_and_b32_e32 v59, 0xffff0000, v60
	v_lshlrev_b32_e32 v60, 16, v61
	v_and_b32_e32 v61, 0xffff0000, v61
	v_and_b32_e32 v65, 0xffff0000, v62
	v_lshlrev_b32_e32 v62, 16, v63
	v_and_b32_e32 v63, 0xffff0000, v63
	v_pk_fma_f32 v[56:57], v[56:57], v[60:61], v[62:63]
	v_pk_fma_f32 v[54:55], v[54:55], v[58:59], v[64:65]
	v_add_u32_e32 v60, 0x90, v144
	v_cvt_pk_bf16_f32 v54, v54, v55
	v_cvt_pk_bf16_f32 v55, v56, v57
	v_mov_b32_e32 v56, v204
	v_mov_b32_e32 v57, v205
	v_mov_b32_e32 v58, v206
	v_mov_b32_e32 v59, v207
	v_ashrrev_i32_e32 v61, 31, v60
	v_mad_i64_i32 v[62:63], s[24:25], v60, s50, v[146:147]
	global_store_dwordx2 v[70:71], v[54:55], off offset:256
	v_lshl_add_u64 v[62:63], v[62:63], 0, v[142:143]
	v_add_co_u32_e32 v64, vcc, s51, v62
	s_nop 0
	v_lshlrev_b32_e32 v54, 16, v56
	v_and_b32_e32 v55, 0xffff0000, v56
	v_lshlrev_b32_e32 v66, 16, v58
	v_and_b32_e32 v67, 0xffff0000, v58
	v_pk_fma_f32 v[50:51], v[50:51], v[54:55], v[66:67]
	v_lshlrev_b64 v[54:55], 12, v[60:61]
	v_lshlrev_b32_e32 v56, 16, v57
	v_and_b32_e32 v57, 0xffff0000, v57
	v_lshlrev_b32_e32 v58, 16, v59
	v_and_b32_e32 v59, 0xffff0000, v59
	v_lshl_add_u64 v[54:55], s[10:11], 0, v[54:55]
	v_addc_co_u32_e32 v65, vcc, 0, v63, vcc
	v_pk_fma_f32 v[52:53], v[52:53], v[56:57], v[58:59]
	v_lshl_add_u64 v[54:55], v[54:55], 0, v[142:143]
	v_cvt_pk_bf16_f32 v50, v50, v51
	v_cvt_pk_bf16_f32 v51, v52, v53
	v_mov_b32_e32 v52, v208
	v_mov_b32_e32 v53, v209
	v_mov_b32_e32 v56, v210
	v_mov_b32_e32 v57, v211
	v_lshl_add_u64 v[58:59], v[62:63], 0, s[12:13]
	global_store_dwordx2 v[70:71], v[50:51], off offset:288
	s_nop 0
	v_lshlrev_b32_e32 v50, 16, v52
	v_and_b32_e32 v51, 0xffff0000, v52
	v_lshlrev_b32_e32 v52, 16, v53
	v_and_b32_e32 v53, 0xffff0000, v53
	v_lshlrev_b32_e32 v60, 16, v56
	v_and_b32_e32 v61, 0xffff0000, v56
	v_lshlrev_b32_e32 v56, 16, v57
	v_and_b32_e32 v57, 0xffff0000, v57
	v_pk_fma_f32 v[48:49], v[48:49], v[52:53], v[56:57]
	v_pk_fma_f32 v[46:47], v[46:47], v[50:51], v[60:61]
	s_nop 0
	v_cvt_pk_bf16_f32 v46, v46, v47
	v_cvt_pk_bf16_f32 v47, v48, v49
	v_mov_b32_e32 v48, v212
	v_mov_b32_e32 v49, v213
	v_mov_b32_e32 v50, v214
	v_mov_b32_e32 v51, v215
	s_nop 0
	v_lshlrev_b32_e32 v52, 16, v50
	global_store_dwordx2 v[54:55], v[46:47], off
	v_lshlrev_b32_e32 v46, 16, v48
	v_and_b32_e32 v47, 0xffff0000, v48
	v_lshlrev_b32_e32 v48, 16, v49
	v_and_b32_e32 v49, 0xffff0000, v49
	v_and_b32_e32 v53, 0xffff0000, v50
	v_lshlrev_b32_e32 v50, 16, v51
	v_and_b32_e32 v51, 0xffff0000, v51
	v_pk_fma_f32 v[44:45], v[44:45], v[48:49], v[50:51]
	v_pk_fma_f32 v[42:43], v[42:43], v[46:47], v[52:53]
	s_nop 0
	v_cvt_pk_bf16_f32 v42, v42, v43
	v_cvt_pk_bf16_f32 v43, v44, v45
	v_mov_b32_e32 v44, v216
	v_mov_b32_e32 v45, v217
	v_mov_b32_e32 v46, v218
	v_mov_b32_e32 v47, v219
	s_nop 0
	v_lshlrev_b32_e32 v48, 16, v46
	global_store_dwordx2 v[54:55], v[42:43], off offset:32
	v_lshlrev_b32_e32 v42, 16, v44
	v_and_b32_e32 v43, 0xffff0000, v44
	v_lshlrev_b32_e32 v44, 16, v45
	v_and_b32_e32 v45, 0xffff0000, v45
	v_and_b32_e32 v49, 0xffff0000, v46
	v_lshlrev_b32_e32 v46, 16, v47
	v_and_b32_e32 v47, 0xffff0000, v47
	v_pk_fma_f32 v[40:41], v[40:41], v[44:45], v[46:47]
	v_pk_fma_f32 v[38:39], v[38:39], v[42:43], v[48:49]
	v_add_u32_e32 v44, 0xa0, v144
	v_cvt_pk_bf16_f32 v38, v38, v39
	v_cvt_pk_bf16_f32 v39, v40, v41
	v_mov_b32_e32 v40, v220
	v_mov_b32_e32 v41, v221
	v_mov_b32_e32 v42, v222
	v_mov_b32_e32 v43, v223
	v_ashrrev_i32_e32 v45, 31, v44
	v_mad_i64_i32 v[46:47], s[24:25], v44, s50, v[146:147]
	global_store_dwordx2 v[54:55], v[38:39], off offset:256
	v_lshl_add_u64 v[46:47], v[46:47], 0, v[142:143]
	v_add_co_u32_e32 v48, vcc, s51, v46
	s_nop 0
	v_lshlrev_b32_e32 v38, 16, v40
	v_and_b32_e32 v39, 0xffff0000, v40
	v_lshlrev_b32_e32 v50, 16, v42
	v_and_b32_e32 v51, 0xffff0000, v42
	v_pk_fma_f32 v[34:35], v[34:35], v[38:39], v[50:51]
	v_lshlrev_b64 v[38:39], 12, v[44:45]
	v_lshlrev_b32_e32 v40, 16, v41
	v_and_b32_e32 v41, 0xffff0000, v41
	v_lshlrev_b32_e32 v42, 16, v43
	v_and_b32_e32 v43, 0xffff0000, v43
	v_lshl_add_u64 v[38:39], s[10:11], 0, v[38:39]
	v_addc_co_u32_e32 v49, vcc, 0, v47, vcc
	v_pk_fma_f32 v[36:37], v[36:37], v[40:41], v[42:43]
	v_lshl_add_u64 v[38:39], v[38:39], 0, v[142:143]
	v_cvt_pk_bf16_f32 v34, v34, v35
	v_cvt_pk_bf16_f32 v35, v36, v37
	v_mov_b32_e32 v237, 0x1000
	v_mov_b32_e32 v236, 160
	v_mad_i64_i32 v[230:231], s[24:25], v236, s50, v[228:229]
	v_mad_i64_i32 v[234:235], s[24:25], v236, v237, v[232:233]
	global_load_dwordx2 v[174:175], v[230:231], off
	global_load_dwordx2 v[176:177], v[234:235], off
	global_load_dwordx2 v[178:179], v[230:231], off offset:32
	global_load_dwordx2 v[180:181], v[234:235], off offset:32
	global_load_dwordx2 v[182:183], v[230:231], off offset:256
	global_load_dwordx2 v[184:185], v[234:235], off offset:256
	global_load_dwordx2 v[186:187], v[230:231], off offset:288
	global_load_dwordx2 v[188:189], v[234:235], off offset:288
	v_mov_b32_e32 v236, 176
	v_mad_i64_i32 v[230:231], s[24:25], v236, s50, v[228:229]
	v_mad_i64_i32 v[234:235], s[24:25], v236, v237, v[232:233]
	global_load_dwordx2 v[192:193], v[230:231], off
	global_load_dwordx2 v[194:195], v[234:235], off
	global_load_dwordx2 v[196:197], v[230:231], off offset:32
	global_load_dwordx2 v[198:199], v[234:235], off offset:32
	global_load_dwordx2 v[200:201], v[230:231], off offset:256
	global_load_dwordx2 v[202:203], v[234:235], off offset:256
	global_load_dwordx2 v[204:205], v[230:231], off offset:288
	global_load_dwordx2 v[206:207], v[234:235], off offset:288
	s_waitcnt vmcnt(0)
	v_mov_b32_e32 v36, v174
	v_mov_b32_e32 v37, v175
	v_mov_b32_e32 v40, v176
	v_mov_b32_e32 v41, v177
	v_lshl_add_u64 v[42:43], v[46:47], 0, s[12:13]
	global_store_dwordx2 v[54:55], v[34:35], off offset:288
	s_nop 0
	v_lshlrev_b32_e32 v34, 16, v36
	v_and_b32_e32 v35, 0xffff0000, v36
	v_lshlrev_b32_e32 v36, 16, v37
	v_and_b32_e32 v37, 0xffff0000, v37
	v_lshlrev_b32_e32 v44, 16, v40
	v_and_b32_e32 v45, 0xffff0000, v40
	v_lshlrev_b32_e32 v40, 16, v41
	v_and_b32_e32 v41, 0xffff0000, v41
	v_pk_fma_f32 v[32:33], v[32:33], v[36:37], v[40:41]
	v_pk_fma_f32 v[30:31], v[30:31], v[34:35], v[44:45]
	s_nop 0
	v_cvt_pk_bf16_f32 v30, v30, v31
	v_cvt_pk_bf16_f32 v31, v32, v33
	v_mov_b32_e32 v32, v178
	v_mov_b32_e32 v33, v179
	v_mov_b32_e32 v34, v180
	v_mov_b32_e32 v35, v181
	s_nop 0
	v_lshlrev_b32_e32 v36, 16, v34
	global_store_dwordx2 v[38:39], v[30:31], off
	v_lshlrev_b32_e32 v30, 16, v32
	v_and_b32_e32 v31, 0xffff0000, v32
	v_lshlrev_b32_e32 v32, 16, v33
	v_and_b32_e32 v33, 0xffff0000, v33
	v_and_b32_e32 v37, 0xffff0000, v34
	v_lshlrev_b32_e32 v34, 16, v35
	v_and_b32_e32 v35, 0xffff0000, v35
	v_pk_fma_f32 v[28:29], v[28:29], v[32:33], v[34:35]
	v_pk_fma_f32 v[26:27], v[26:27], v[30:31], v[36:37]
	s_nop 0
	v_cvt_pk_bf16_f32 v26, v26, v27
	v_cvt_pk_bf16_f32 v27, v28, v29
	v_mov_b32_e32 v28, v182
	v_mov_b32_e32 v29, v183
	v_mov_b32_e32 v30, v184
	v_mov_b32_e32 v31, v185
	s_nop 0
	v_lshlrev_b32_e32 v32, 16, v30
	global_store_dwordx2 v[38:39], v[26:27], off offset:32
	v_lshlrev_b32_e32 v26, 16, v28
	v_and_b32_e32 v27, 0xffff0000, v28
	v_lshlrev_b32_e32 v28, 16, v29
	v_and_b32_e32 v29, 0xffff0000, v29
	v_and_b32_e32 v33, 0xffff0000, v30
	v_lshlrev_b32_e32 v30, 16, v31
	v_and_b32_e32 v31, 0xffff0000, v31
	v_pk_fma_f32 v[24:25], v[24:25], v[28:29], v[30:31]
	v_pk_fma_f32 v[22:23], v[22:23], v[26:27], v[32:33]
	v_add_u32_e32 v28, 0xb0, v144
	v_cvt_pk_bf16_f32 v22, v22, v23
	v_cvt_pk_bf16_f32 v23, v24, v25
	v_mov_b32_e32 v24, v186
	v_mov_b32_e32 v25, v187
	v_mov_b32_e32 v26, v188
	v_mov_b32_e32 v27, v189
	v_ashrrev_i32_e32 v29, 31, v28
	v_mad_i64_i32 v[30:31], s[24:25], v28, s50, v[146:147]
	global_store_dwordx2 v[38:39], v[22:23], off offset:256
	v_lshl_add_u64 v[30:31], v[30:31], 0, v[142:143]
	v_add_co_u32_e32 v32, vcc, s51, v30
	s_mov_b64 s[24:25], s[18:19]
	s_nop 0
	v_addc_co_u32_e32 v33, vcc, 0, v31, vcc
	s_and_b64 vcc, exec, s[2:3]
	s_nop 0
	v_lshlrev_b32_e32 v22, 16, v24
	v_and_b32_e32 v23, 0xffff0000, v24
	v_lshlrev_b32_e32 v34, 16, v26
	v_and_b32_e32 v35, 0xffff0000, v26
	v_pk_fma_f32 v[18:19], v[18:19], v[22:23], v[34:35]
	v_lshlrev_b64 v[22:23], 12, v[28:29]
	v_lshlrev_b32_e32 v24, 16, v25
	v_and_b32_e32 v25, 0xffff0000, v25
	v_lshlrev_b32_e32 v26, 16, v27
	v_and_b32_e32 v27, 0xffff0000, v27
	v_lshl_add_u64 v[22:23], s[10:11], 0, v[22:23]
	v_pk_fma_f32 v[20:21], v[20:21], v[24:25], v[26:27]
	v_lshl_add_u64 v[22:23], v[22:23], 0, v[142:143]
	v_cvt_pk_bf16_f32 v18, v18, v19
	v_cvt_pk_bf16_f32 v19, v20, v21
	v_mov_b32_e32 v20, v192
	v_mov_b32_e32 v21, v193
	v_mov_b32_e32 v24, v194
	v_mov_b32_e32 v25, v195
	v_lshl_add_u64 v[26:27], v[30:31], 0, s[12:13]
	global_store_dwordx2 v[38:39], v[18:19], off offset:288
	s_nop 0
	v_lshlrev_b32_e32 v18, 16, v20
	v_and_b32_e32 v19, 0xffff0000, v20
	v_lshlrev_b32_e32 v20, 16, v21
	v_and_b32_e32 v21, 0xffff0000, v21
	v_lshlrev_b32_e32 v28, 16, v24
	v_and_b32_e32 v29, 0xffff0000, v24
	v_lshlrev_b32_e32 v24, 16, v25
	v_and_b32_e32 v25, 0xffff0000, v25
	v_pk_fma_f32 v[16:17], v[16:17], v[20:21], v[24:25]
	v_pk_fma_f32 v[14:15], v[14:15], v[18:19], v[28:29]
	s_nop 0
	v_cvt_pk_bf16_f32 v14, v14, v15
	v_cvt_pk_bf16_f32 v15, v16, v17
	v_mov_b32_e32 v16, v196
	v_mov_b32_e32 v17, v197
	v_mov_b32_e32 v18, v198
	v_mov_b32_e32 v19, v199
	s_nop 0
	v_lshlrev_b32_e32 v20, 16, v18
	global_store_dwordx2 v[22:23], v[14:15], off
	v_lshlrev_b32_e32 v14, 16, v16
	v_and_b32_e32 v15, 0xffff0000, v16
	v_lshlrev_b32_e32 v16, 16, v17
	v_and_b32_e32 v17, 0xffff0000, v17
	v_and_b32_e32 v21, 0xffff0000, v18
	v_lshlrev_b32_e32 v18, 16, v19
	v_and_b32_e32 v19, 0xffff0000, v19
	v_pk_fma_f32 v[12:13], v[12:13], v[16:17], v[18:19]
	v_pk_fma_f32 v[10:11], v[10:11], v[14:15], v[20:21]
	s_nop 0
	v_cvt_pk_bf16_f32 v10, v10, v11
	v_cvt_pk_bf16_f32 v11, v12, v13
	v_mov_b32_e32 v12, v200
	v_mov_b32_e32 v13, v201
	v_mov_b32_e32 v14, v202
	v_mov_b32_e32 v15, v203
	s_nop 0
	v_lshlrev_b32_e32 v16, 16, v14
	global_store_dwordx2 v[22:23], v[10:11], off offset:32
	v_lshlrev_b32_e32 v10, 16, v12
	v_and_b32_e32 v11, 0xffff0000, v12
	v_lshlrev_b32_e32 v12, 16, v13
	v_and_b32_e32 v13, 0xffff0000, v13
	v_and_b32_e32 v17, 0xffff0000, v14
	v_lshlrev_b32_e32 v14, 16, v15
	v_and_b32_e32 v15, 0xffff0000, v15
	v_pk_fma_f32 v[8:9], v[8:9], v[12:13], v[14:15]
	v_pk_fma_f32 v[6:7], v[6:7], v[10:11], v[16:17]
	s_nop 0
	v_cvt_pk_bf16_f32 v6, v6, v7
	v_cvt_pk_bf16_f32 v7, v8, v9
	v_mov_b32_e32 v8, v204
	v_mov_b32_e32 v9, v205
	v_mov_b32_e32 v10, v206
	v_mov_b32_e32 v11, v207
	s_nop 0
	v_lshlrev_b32_e32 v12, 16, v10
	global_store_dwordx2 v[22:23], v[6:7], off offset:256
	v_lshlrev_b32_e32 v6, 16, v8
	v_and_b32_e32 v7, 0xffff0000, v8
	v_and_b32_e32 v13, 0xffff0000, v10
	v_lshlrev_b32_e32 v8, 16, v9
	v_and_b32_e32 v9, 0xffff0000, v9
	v_lshlrev_b32_e32 v10, 16, v11
	v_and_b32_e32 v11, 0xffff0000, v11
	v_pk_fma_f32 v[2:3], v[2:3], v[6:7], v[12:13]
	v_pk_fma_f32 v[4:5], v[4:5], v[8:9], v[10:11]
	v_cvt_pk_bf16_f32 v2, v2, v3
	s_nop 0
	v_cvt_pk_bf16_f32 v3, v4, v5
	global_store_dwordx2 v[22:23], v[2:3], off offset:288
	s_cbranch_vccz .LBB0_1208
	s_waitcnt vmcnt(0)
	v_readlane_b32 s52, v250, 40
	s_cmpk_gt_u32 s33, 0xff
	v_readlane_b32 s53, v250, 41
	v_readlane_b32 s54, v250, 42
	v_readlane_b32 s55, v250, 43
	s_cbranch_scc1 .LBB0_1215
	s_barrier

.LBB0_1223:
	ds_read_b128 v[142:145], v1
	ds_read_b128 v[156:159], v1 offset:1024
	ds_read_b128 v[160:163], v1 offset:2048
	ds_read_b128 v[164:167], v1 offset:3072
	s_add_u32 s24, s22, 0xfffc0080
	s_addc_u32 s25, s23, -1
	s_cmp_eq_u32 s55, 12
	s_cselect_b32 s27, s15, s25
	s_cselect_b32 s26, s51, s24
	s_cselect_b32 s25, s13, s54
	s_cselect_b32 s24, s52, s53
	v_lshl_add_u64 v[146:147], s[22:23], 0, v[134:135]
	s_add_i32 m0, s21, 0xc000
	ds_read_b128 v[168:171], v148
	ds_read_b128 v[172:175], v148 offset:1024
	ds_read_b128 v[176:179], v148 offset:2048
	ds_read_b128 v[180:183], v148 offset:3072
	ds_read_b128 v[184:187], v148 offset:4096
	ds_read_b128 v[192:195], v148 offset:5120
	ds_read_b128 v[196:199], v148 offset:6144
	ds_read_b128 v[200:203], v148 offset:7168
	global_load_lds_dwordx4 v[146:147], off
	v_lshl_add_u64 v[146:147], s[22:23], 0, v[136:137]
	s_add_i32 m0, s21, 0xe000
	s_nop 0
	global_load_lds_dwordx4 v[146:147], off
	s_waitcnt lgkmcnt(8)
	s_barrier
	s_waitcnt lgkmcnt(0)
	s_setprio 1
	s_waitcnt lgkmcnt(0)
	v_mfma_f32_16x16x32_bf16 v[126:129], v[142:145], v[168:171], v[126:129]
	v_mfma_f32_16x16x32_bf16 v[122:125], v[160:163], v[168:171], v[122:125]
	v_mfma_f32_16x16x32_bf16 v[110:113], v[142:145], v[176:179], v[110:113]
	v_mfma_f32_16x16x32_bf16 v[106:109], v[160:163], v[176:179], v[106:109]
	v_mfma_f32_16x16x32_bf16 v[94:97], v[142:145], v[184:187], v[94:97]
	v_mfma_f32_16x16x32_bf16 v[90:93], v[160:163], v[184:187], v[90:93]
	v_mfma_f32_16x16x32_bf16 v[78:81], v[142:145], v[196:199], v[78:81]
	v_mfma_f32_16x16x32_bf16 v[74:77], v[160:163], v[196:199], v[74:77]
	v_mfma_f32_16x16x32_bf16 v[126:129], v[156:159], v[172:175], v[126:129]
	v_mfma_f32_16x16x32_bf16 v[122:125], v[164:167], v[172:175], v[122:125]
	v_mfma_f32_16x16x32_bf16 v[110:113], v[156:159], v[180:183], v[110:113]
	v_mfma_f32_16x16x32_bf16 v[106:109], v[164:167], v[180:183], v[106:109]
	v_mfma_f32_16x16x32_bf16 v[94:97], v[156:159], v[192:195], v[94:97]
	v_mfma_f32_16x16x32_bf16 v[90:93], v[164:167], v[192:195], v[90:93]
	v_mfma_f32_16x16x32_bf16 v[78:81], v[156:159], v[200:203], v[78:81]
	v_mfma_f32_16x16x32_bf16 v[74:77], v[164:167], v[200:203], v[74:77]
	s_setprio 0
	s_barrier
	s_add_i32 s56, s46, s36
	v_lshl_add_u64 v[146:147], s[24:25], 0, v[130:131]
	s_mov_b32 m0, s56
	ds_read_b128 v[204:207], v149
	ds_read_b128 v[208:211], v149 offset:1024
	ds_read_b128 v[212:215], v149 offset:2048
	ds_read_b128 v[216:219], v149 offset:3072
	global_load_lds_dwordx4 v[146:147], off
	v_lshl_add_u64 v[188:189], s[24:25], 0, v[132:133]
	s_add_i32 m0, s56, 0x2000
	s_nop 0
	global_load_lds_dwordx4 v[188:189], off
	s_barrier
	s_waitcnt lgkmcnt(0)
	s_setprio 1
	s_waitcnt lgkmcnt(0)
	v_mfma_f32_16x16x32_bf16 v[118:121], v[204:207], v[168:171], v[118:121]
	v_mfma_f32_16x16x32_bf16 v[114:117], v[212:215], v[168:171], v[114:117]
	v_mfma_f32_16x16x32_bf16 v[102:105], v[204:207], v[176:179], v[102:105]
	v_mfma_f32_16x16x32_bf16 v[98:101], v[212:215], v[176:179], v[98:101]
	v_mfma_f32_16x16x32_bf16 v[86:89], v[204:207], v[184:187], v[86:89]
	v_mfma_f32_16x16x32_bf16 v[82:85], v[212:215], v[184:187], v[82:85]
	v_mfma_f32_16x16x32_bf16 v[70:73], v[204:207], v[196:199], v[70:73]
	v_mfma_f32_16x16x32_bf16 v[66:69], v[212:215], v[196:199], v[66:69]
	v_mfma_f32_16x16x32_bf16 v[118:121], v[208:211], v[172:175], v[118:121]
	v_mfma_f32_16x16x32_bf16 v[114:117], v[216:219], v[172:175], v[114:117]
	v_mfma_f32_16x16x32_bf16 v[102:105], v[208:211], v[180:183], v[102:105]
	v_mfma_f32_16x16x32_bf16 v[98:101], v[216:219], v[180:183], v[98:101]
	v_mfma_f32_16x16x32_bf16 v[86:89], v[208:211], v[192:195], v[86:89]
	v_mfma_f32_16x16x32_bf16 v[82:85], v[216:219], v[192:195], v[82:85]
	v_mfma_f32_16x16x32_bf16 v[70:73], v[208:211], v[200:203], v[70:73]
	v_mfma_f32_16x16x32_bf16 v[66:69], v[216:219], v[200:203], v[66:69]
	s_setprio 0
	s_mov_b32 m0, s21
	v_lshl_add_u64 v[190:191], s[26:27], 0, v[130:131]
	s_barrier
	ds_read_b128 v[168:171], v148 offset:16384
	ds_read_b128 v[172:175], v148 offset:17408
	ds_read_b128 v[176:179], v148 offset:18432
	ds_read_b128 v[180:183], v148 offset:19456
	ds_read_b128 v[184:187], v148 offset:20480
	ds_read_b128 v[192:195], v148 offset:21504
	ds_read_b128 v[196:199], v148 offset:22528
	ds_read_b128 v[200:203], v148 offset:23552
	global_load_lds_dwordx4 v[190:191], off
	v_lshl_add_u64 v[220:221], s[26:27], 0, v[132:133]
	s_mov_b32 m0, s39
	s_nop 0
	global_load_lds_dwordx4 v[220:221], off
	s_barrier
	s_waitcnt lgkmcnt(0)
	s_setprio 1
	s_waitcnt lgkmcnt(0)
	v_mfma_f32_16x16x32_bf16 v[62:65], v[142:145], v[168:171], v[62:65]
	v_mfma_f32_16x16x32_bf16 v[58:61], v[160:163], v[168:171], v[58:61]
	v_mfma_f32_16x16x32_bf16 v[46:49], v[142:145], v[176:179], v[46:49]
	v_mfma_f32_16x16x32_bf16 v[42:45], v[160:163], v[176:179], v[42:45]
	v_mfma_f32_16x16x32_bf16 v[30:33], v[142:145], v[184:187], v[30:33]
	v_mfma_f32_16x16x32_bf16 v[26:29], v[160:163], v[184:187], v[26:29]
	v_mfma_f32_16x16x32_bf16 v[14:17], v[142:145], v[196:199], v[14:17]
	v_mfma_f32_16x16x32_bf16 v[10:13], v[160:163], v[196:199], v[10:13]
	v_mfma_f32_16x16x32_bf16 v[62:65], v[156:159], v[172:175], v[62:65]
	v_mfma_f32_16x16x32_bf16 v[58:61], v[164:167], v[172:175], v[58:61]
	v_mfma_f32_16x16x32_bf16 v[46:49], v[156:159], v[180:183], v[46:49]
	v_mfma_f32_16x16x32_bf16 v[42:45], v[164:167], v[180:183], v[42:45]
	v_mfma_f32_16x16x32_bf16 v[30:33], v[156:159], v[192:195], v[30:33]
	v_mfma_f32_16x16x32_bf16 v[26:29], v[164:167], v[192:195], v[26:29]
	v_mfma_f32_16x16x32_bf16 v[14:17], v[156:159], v[200:203], v[14:17]
	v_mfma_f32_16x16x32_bf16 v[10:13], v[164:167], v[200:203], v[10:13]
	s_setprio 0
	s_barrier
	s_add_u32 s56, s24, 0x40000
	s_addc_u32 s57, s25, 0
	s_add_i32 s58, s47, s36
	v_lshl_add_u64 v[142:143], s[56:57], 0, v[130:131]
	s_mov_b32 m0, s58
	s_nop 0
	global_load_lds_dwordx4 v[142:143], off
	v_lshl_add_u64 v[142:143], s[56:57], 0, v[132:133]
	s_add_i32 m0, s58, 0x2000
	s_nop 0
	global_load_lds_dwordx4 v[142:143], off
	s_waitcnt vmcnt(6)
	s_barrier
	s_setprio 1
	v_mfma_f32_16x16x32_bf16 v[54:57], v[204:207], v[168:171], v[54:57]
	v_mfma_f32_16x16x32_bf16 v[50:53], v[212:215], v[168:171], v[50:53]
	v_mfma_f32_16x16x32_bf16 v[38:41], v[204:207], v[176:179], v[38:41]
	v_mfma_f32_16x16x32_bf16 v[34:37], v[212:215], v[176:179], v[34:37]
	v_mfma_f32_16x16x32_bf16 v[22:25], v[204:207], v[184:187], v[22:25]
	v_mfma_f32_16x16x32_bf16 v[18:21], v[212:215], v[184:187], v[18:21]
	v_mfma_f32_16x16x32_bf16 v[6:9], v[204:207], v[196:199], v[6:9]
	v_mfma_f32_16x16x32_bf16 v[2:5], v[212:215], v[196:199], v[2:5]
	v_mfma_f32_16x16x32_bf16 v[54:57], v[208:211], v[172:175], v[54:57]
	v_mfma_f32_16x16x32_bf16 v[50:53], v[216:219], v[172:175], v[50:53]
	v_mfma_f32_16x16x32_bf16 v[38:41], v[208:211], v[180:183], v[38:41]
	v_mfma_f32_16x16x32_bf16 v[34:37], v[216:219], v[180:183], v[34:37]
	v_mfma_f32_16x16x32_bf16 v[22:25], v[208:211], v[192:195], v[22:25]
	v_mfma_f32_16x16x32_bf16 v[18:21], v[216:219], v[192:195], v[18:21]
	v_mfma_f32_16x16x32_bf16 v[6:9], v[208:211], v[200:203], v[6:9]
	v_mfma_f32_16x16x32_bf16 v[2:5], v[216:219], v[200:203], v[2:5]
	s_setprio 0
	s_add_i32 s56, 0, 0x18000
	v_add_u32_e32 v150, s56, v152
	s_barrier
	ds_read_b128 v[142:145], v150
	ds_read_b128 v[156:159], v150 offset:1024
	ds_read_b128 v[160:163], v150 offset:2048
	ds_read_b128 v[164:167], v150 offset:3072
	s_add_u32 s26, s26, 0x40000
	s_addc_u32 s27, s27, 0
	s_mov_b32 m0, s40
	v_lshl_add_u64 v[204:205], s[26:27], 0, v[130:131]
	ds_read_b128 v[168:171], v148 offset:32768
	ds_read_b128 v[172:175], v148 offset:33792
	ds_read_b128 v[176:179], v148 offset:34816
	ds_read_b128 v[180:183], v148 offset:35840
	ds_read_b128 v[184:187], v148 offset:36864
	ds_read_b128 v[192:195], v148 offset:37888
	ds_read_b128 v[196:199], v148 offset:38912
	ds_read_b128 v[200:203], v148 offset:39936
	global_load_lds_dwordx4 v[204:205], off
	v_lshl_add_u64 v[204:205], s[26:27], 0, v[132:133]
	s_mov_b32 m0, s41
	s_nop 0
	global_load_lds_dwordx4 v[204:205], off
	s_waitcnt lgkmcnt(8)
	s_barrier
	s_waitcnt lgkmcnt(0)
	s_setprio 1
	s_waitcnt lgkmcnt(0)
	v_mfma_f32_16x16x32_bf16 v[126:129], v[142:145], v[168:171], v[126:129]
	v_mfma_f32_16x16x32_bf16 v[122:125], v[160:163], v[168:171], v[122:125]
	v_mfma_f32_16x16x32_bf16 v[110:113], v[142:145], v[176:179], v[110:113]
	v_mfma_f32_16x16x32_bf16 v[106:109], v[160:163], v[176:179], v[106:109]
	v_mfma_f32_16x16x32_bf16 v[94:97], v[142:145], v[184:187], v[94:97]
	v_mfma_f32_16x16x32_bf16 v[90:93], v[160:163], v[184:187], v[90:93]
	v_mfma_f32_16x16x32_bf16 v[78:81], v[142:145], v[196:199], v[78:81]
	v_mfma_f32_16x16x32_bf16 v[74:77], v[160:163], v[196:199], v[74:77]
	v_mfma_f32_16x16x32_bf16 v[126:129], v[156:159], v[172:175], v[126:129]
	v_mfma_f32_16x16x32_bf16 v[122:125], v[164:167], v[172:175], v[122:125]
	v_mfma_f32_16x16x32_bf16 v[110:113], v[156:159], v[180:183], v[110:113]
	v_mfma_f32_16x16x32_bf16 v[106:109], v[164:167], v[180:183], v[106:109]
	v_mfma_f32_16x16x32_bf16 v[94:97], v[156:159], v[192:195], v[94:97]
	v_mfma_f32_16x16x32_bf16 v[90:93], v[164:167], v[192:195], v[90:93]
	v_mfma_f32_16x16x32_bf16 v[78:81], v[156:159], v[200:203], v[78:81]
	v_mfma_f32_16x16x32_bf16 v[74:77], v[164:167], v[200:203], v[74:77]
	s_setprio 0
	s_barrier
	s_add_i32 s26, 0, 0x1c000
	s_add_i32 s27, s56, s36
	v_add_u32_e32 v150, s26, v152
	v_lshl_add_u64 v[146:147], v[146:147], 0, s[2:3]
	s_mov_b32 m0, s27
	ds_read_b128 v[204:207], v150
	ds_read_b128 v[208:211], v150 offset:1024
	ds_read_b128 v[212:215], v150 offset:2048
	ds_read_b128 v[216:219], v150 offset:3072
	global_load_lds_dwordx4 v[146:147], off
	v_lshl_add_u64 v[146:147], v[188:189], 0, s[2:3]
	s_add_i32 m0, s27, 0x2000
	s_nop 0
	global_load_lds_dwordx4 v[146:147], off
	s_barrier
	s_waitcnt lgkmcnt(0)
	s_setprio 1
	s_waitcnt lgkmcnt(0)
	v_mfma_f32_16x16x32_bf16 v[118:121], v[204:207], v[168:171], v[118:121]
	v_mfma_f32_16x16x32_bf16 v[114:117], v[212:215], v[168:171], v[114:117]
	v_mfma_f32_16x16x32_bf16 v[102:105], v[204:207], v[176:179], v[102:105]
	v_mfma_f32_16x16x32_bf16 v[98:101], v[212:215], v[176:179], v[98:101]
	v_mfma_f32_16x16x32_bf16 v[86:89], v[204:207], v[184:187], v[86:89]
	v_mfma_f32_16x16x32_bf16 v[82:85], v[212:215], v[184:187], v[82:85]
	v_mfma_f32_16x16x32_bf16 v[70:73], v[204:207], v[196:199], v[70:73]
	v_mfma_f32_16x16x32_bf16 v[66:69], v[212:215], v[196:199], v[66:69]
	v_mfma_f32_16x16x32_bf16 v[118:121], v[208:211], v[172:175], v[118:121]
	v_mfma_f32_16x16x32_bf16 v[114:117], v[216:219], v[172:175], v[114:117]
	v_mfma_f32_16x16x32_bf16 v[102:105], v[208:211], v[180:183], v[102:105]
	v_mfma_f32_16x16x32_bf16 v[98:101], v[216:219], v[180:183], v[98:101]
	v_mfma_f32_16x16x32_bf16 v[86:89], v[208:211], v[192:195], v[86:89]
	v_mfma_f32_16x16x32_bf16 v[82:85], v[216:219], v[192:195], v[82:85]
	v_mfma_f32_16x16x32_bf16 v[70:73], v[208:211], v[200:203], v[70:73]
	v_mfma_f32_16x16x32_bf16 v[66:69], v[216:219], v[200:203], v[66:69]
	s_setprio 0
	s_mov_b32 m0, s43
	v_lshl_add_u64 v[146:147], v[190:191], 0, s[2:3]
	s_barrier
	ds_read_b128 v[168:171], v148 offset:49152
	ds_read_b128 v[172:175], v148 offset:50176
	ds_read_b128 v[176:179], v148 offset:51200
	ds_read_b128 v[180:183], v148 offset:52224
	ds_read_b128 v[184:187], v148 offset:53248
	ds_read_b128 v[192:195], v148 offset:54272
	ds_read_b128 v[196:199], v148 offset:55296
	ds_read_b128 v[200:203], v148 offset:56320
	global_load_lds_dwordx4 v[146:147], off
	v_lshl_add_u64 v[146:147], v[220:221], 0, s[2:3]
	s_mov_b32 m0, s44
	s_nop 0
	global_load_lds_dwordx4 v[146:147], off
	s_barrier
	s_waitcnt lgkmcnt(0)
	s_setprio 1
	s_waitcnt lgkmcnt(0)
	v_mfma_f32_16x16x32_bf16 v[62:65], v[142:145], v[168:171], v[62:65]
	v_mfma_f32_16x16x32_bf16 v[58:61], v[160:163], v[168:171], v[58:61]
	v_mfma_f32_16x16x32_bf16 v[46:49], v[142:145], v[176:179], v[46:49]
	v_mfma_f32_16x16x32_bf16 v[42:45], v[160:163], v[176:179], v[42:45]
	v_mfma_f32_16x16x32_bf16 v[30:33], v[142:145], v[184:187], v[30:33]
	v_mfma_f32_16x16x32_bf16 v[26:29], v[160:163], v[184:187], v[26:29]
	v_mfma_f32_16x16x32_bf16 v[14:17], v[142:145], v[196:199], v[14:17]
	v_mfma_f32_16x16x32_bf16 v[10:13], v[160:163], v[196:199], v[10:13]
	v_mfma_f32_16x16x32_bf16 v[62:65], v[156:159], v[172:175], v[62:65]
	v_mfma_f32_16x16x32_bf16 v[58:61], v[164:167], v[172:175], v[58:61]
	v_mfma_f32_16x16x32_bf16 v[46:49], v[156:159], v[180:183], v[46:49]
	v_mfma_f32_16x16x32_bf16 v[42:45], v[164:167], v[180:183], v[42:45]
	v_mfma_f32_16x16x32_bf16 v[30:33], v[156:159], v[192:195], v[30:33]
	v_mfma_f32_16x16x32_bf16 v[26:29], v[164:167], v[192:195], v[26:29]
	v_mfma_f32_16x16x32_bf16 v[14:17], v[156:159], v[200:203], v[14:17]
	v_mfma_f32_16x16x32_bf16 v[10:13], v[164:167], v[200:203], v[10:13]
	s_setprio 0
	s_barrier
	s_add_u32 s24, s24, 0x40080
	s_addc_u32 s25, s25, 0
	s_add_i32 s26, s26, s36
	v_lshl_add_u64 v[142:143], s[24:25], 0, v[130:131]
	s_mov_b32 m0, s26
	s_nop 0
	global_load_lds_dwordx4 v[142:143], off
	v_lshl_add_u64 v[142:143], s[24:25], 0, v[132:133]
	s_add_i32 m0, s26, 0x2000
	s_nop 0
	global_load_lds_dwordx4 v[142:143], off
	s_waitcnt vmcnt(6)
	s_barrier
	s_setprio 1
	v_mfma_f32_16x16x32_bf16 v[54:57], v[204:207], v[168:171], v[54:57]
	v_mfma_f32_16x16x32_bf16 v[50:53], v[212:215], v[168:171], v[50:53]
	v_mfma_f32_16x16x32_bf16 v[38:41], v[204:207], v[176:179], v[38:41]
	v_mfma_f32_16x16x32_bf16 v[34:37], v[212:215], v[176:179], v[34:37]
	v_mfma_f32_16x16x32_bf16 v[22:25], v[204:207], v[184:187], v[22:25]
	v_mfma_f32_16x16x32_bf16 v[18:21], v[212:215], v[184:187], v[18:21]
	v_mfma_f32_16x16x32_bf16 v[6:9], v[204:207], v[196:199], v[6:9]
	v_mfma_f32_16x16x32_bf16 v[2:5], v[212:215], v[196:199], v[2:5]
	v_mfma_f32_16x16x32_bf16 v[54:57], v[208:211], v[172:175], v[54:57]
	v_mfma_f32_16x16x32_bf16 v[50:53], v[216:219], v[172:175], v[50:53]
	v_mfma_f32_16x16x32_bf16 v[38:41], v[208:211], v[180:183], v[38:41]
	v_mfma_f32_16x16x32_bf16 v[34:37], v[216:219], v[180:183], v[34:37]
	v_mfma_f32_16x16x32_bf16 v[22:25], v[208:211], v[192:195], v[22:25]
	v_mfma_f32_16x16x32_bf16 v[18:21], v[216:219], v[192:195], v[18:21]
	v_mfma_f32_16x16x32_bf16 v[6:9], v[208:211], v[200:203], v[6:9]
	v_mfma_f32_16x16x32_bf16 v[2:5], v[216:219], v[200:203], v[2:5]
	s_setprio 0
	s_add_i32 s55, s55, 2
	s_add_u32 s22, s22, 0x100
	s_addc_u32 s23, s23, 0
	s_add_u32 s53, s53, 0x100
	s_addc_u32 s54, s54, 0
	s_cmp_gt_u32 s55, 13
	s_barrier
	s_cbranch_scc0 .LBB0_1223
	v_lshl_or_b32 v142, s50, 8, v151
	v_lshl_add_u32 v144, s20, 8, v155
	v_ashrrev_i32_e32 v143, 31, v142
	v_mov_b64_e32 v[146:147], s[6:7]
	v_ashrrev_i32_e32 v145, 31, v144
	v_mad_i64_i32 v[156:157], s[22:23], v144, s48, v[146:147]
	v_lshlrev_b64 v[142:143], 1, v[142:143]
	v_lshl_add_u64 v[156:157], v[156:157], 0, v[142:143]
	v_lshlrev_b64 v[160:161], 12, v[144:145]
	v_add_co_u32_e32 v158, vcc, 0x2ec42000, v156
	v_lshl_add_u64 v[160:161], s[8:9], 0, v[160:161]
	s_nop 0
	v_addc_co_u32_e32 v159, vcc, 0, v157, vcc
	v_lshl_add_u64 v[160:161], v[160:161], 0, v[142:143]
	v_mov_b32_e32 v228, v158
	v_mov_b32_e32 v229, v159
	v_mov_b32_e32 v232, v160
	v_mov_b32_e32 v233, v161
	v_mov_b32_e32 v237, 0x1000
	global_load_dwordx2 v[168:169], v[228:229], off
	global_load_dwordx2 v[170:171], v[232:233], off
	global_load_dwordx2 v[172:173], v[228:229], off offset:32
	global_load_dwordx2 v[174:175], v[232:233], off offset:32
	global_load_dwordx2 v[176:177], v[228:229], off offset:256
	global_load_dwordx2 v[178:179], v[232:233], off offset:256
	global_load_dwordx2 v[180:181], v[228:229], off offset:288
	global_load_dwordx2 v[182:183], v[232:233], off offset:288
	v_mov_b32_e32 v236, 16
	v_mad_i64_i32 v[230:231], s[22:23], v236, s48, v[228:229]
	v_mad_i64_i32 v[234:235], s[22:23], v236, v237, v[232:233]
	global_load_dwordx2 v[184:185], v[230:231], off
	global_load_dwordx2 v[186:187], v[234:235], off
	global_load_dwordx2 v[192:193], v[230:231], off offset:32
	global_load_dwordx2 v[194:195], v[234:235], off offset:32
	global_load_dwordx2 v[196:197], v[230:231], off offset:256
	global_load_dwordx2 v[198:199], v[234:235], off offset:256
	global_load_dwordx2 v[200:201], v[230:231], off offset:288
	global_load_dwordx2 v[202:203], v[234:235], off offset:288
	v_mov_b32_e32 v236, 32
	v_mad_i64_i32 v[230:231], s[22:23], v236, s48, v[228:229]
	v_mad_i64_i32 v[234:235], s[22:23], v236, v237, v[232:233]
	global_load_dwordx2 v[204:205], v[230:231], off
	global_load_dwordx2 v[206:207], v[234:235], off
	global_load_dwordx2 v[208:209], v[230:231], off offset:32
	global_load_dwordx2 v[210:211], v[234:235], off offset:32
	global_load_dwordx2 v[212:213], v[230:231], off offset:256
	global_load_dwordx2 v[214:215], v[234:235], off offset:256
	global_load_dwordx2 v[216:217], v[230:231], off offset:288
	global_load_dwordx2 v[218:219], v[234:235], off offset:288
	s_waitcnt vmcnt(0)
	v_mov_b32_e32 v158, v168
	v_mov_b32_e32 v159, v169
	v_lshl_add_u64 v[156:157], v[156:157], 0, s[10:11]
	v_mov_b32_e32 v162, v170
	v_mov_b32_e32 v163, v171
	s_mov_b32 s50, s12
	s_mov_b32 s20, s14
	s_mov_b64 s[24:25], s[18:19]
	s_nop 0
	v_lshlrev_b32_e32 v164, 16, v158
	v_and_b32_e32 v165, 0xffff0000, v158
	v_lshlrev_b32_e32 v158, 16, v159
	v_and_b32_e32 v159, 0xffff0000, v159
	v_lshlrev_b32_e32 v166, 16, v162
	v_and_b32_e32 v167, 0xffff0000, v162
	v_lshlrev_b32_e32 v162, 16, v163
	v_and_b32_e32 v163, 0xffff0000, v163
	v_pk_fma_f32 v[128:129], v[128:129], v[158:159], v[162:163]
	v_pk_fma_f32 v[126:127], v[126:127], v[164:165], v[166:167]
	s_nop 0
	v_cvt_pk_bf16_f32 v126, v126, v127
	v_cvt_pk_bf16_f32 v127, v128, v129
	v_mov_b32_e32 v128, v172
	v_mov_b32_e32 v129, v173
	v_mov_b32_e32 v158, v174
	v_mov_b32_e32 v159, v175
	s_nop 0
	v_lshlrev_b32_e32 v162, 16, v158
	global_store_dwordx2 v[160:161], v[126:127], off
	v_lshlrev_b32_e32 v126, 16, v128
	v_and_b32_e32 v127, 0xffff0000, v128
	v_lshlrev_b32_e32 v128, 16, v129
	v_and_b32_e32 v129, 0xffff0000, v129
	v_and_b32_e32 v163, 0xffff0000, v158
	v_lshlrev_b32_e32 v158, 16, v159
	v_and_b32_e32 v159, 0xffff0000, v159
	v_pk_fma_f32 v[124:125], v[124:125], v[128:129], v[158:159]
	v_pk_fma_f32 v[122:123], v[122:123], v[126:127], v[162:163]
	s_nop 0
	v_cvt_pk_bf16_f32 v122, v122, v123
	v_cvt_pk_bf16_f32 v123, v124, v125
	v_mov_b32_e32 v124, v176
	v_mov_b32_e32 v125, v177
	v_mov_b32_e32 v126, v178
	v_mov_b32_e32 v127, v179
	s_nop 0
	v_lshlrev_b32_e32 v128, 16, v126
	global_store_dwordx2 v[160:161], v[122:123], off offset:32
	v_lshlrev_b32_e32 v122, 16, v124
	v_and_b32_e32 v123, 0xffff0000, v124
	v_lshlrev_b32_e32 v124, 16, v125
	v_and_b32_e32 v125, 0xffff0000, v125
	v_and_b32_e32 v129, 0xffff0000, v126
	v_lshlrev_b32_e32 v126, 16, v127
	v_and_b32_e32 v127, 0xffff0000, v127
	v_pk_fma_f32 v[120:121], v[120:121], v[124:125], v[126:127]
	v_pk_fma_f32 v[118:119], v[118:119], v[122:123], v[128:129]
	v_or_b32_e32 v124, 16, v144
	v_cvt_pk_bf16_f32 v118, v118, v119
	v_cvt_pk_bf16_f32 v119, v120, v121
	v_mov_b32_e32 v120, v180
	v_mov_b32_e32 v121, v181
	v_mov_b32_e32 v122, v182
	v_mov_b32_e32 v123, v183
	v_ashrrev_i32_e32 v125, 31, v124
	v_mad_i64_i32 v[126:127], s[22:23], v124, s48, v[146:147]
	global_store_dwordx2 v[160:161], v[118:119], off offset:256
	v_lshl_add_u64 v[126:127], v[126:127], 0, v[142:143]
	v_add_co_u32_e32 v128, vcc, s49, v126
	s_nop 0
	v_lshlrev_b32_e32 v118, 16, v120
	v_and_b32_e32 v119, 0xffff0000, v120
	v_lshlrev_b32_e32 v156, 16, v122
	v_and_b32_e32 v157, 0xffff0000, v122
	v_pk_fma_f32 v[114:115], v[114:115], v[118:119], v[156:157]
	v_lshlrev_b64 v[118:119], 12, v[124:125]
	v_lshlrev_b32_e32 v120, 16, v121
	v_and_b32_e32 v121, 0xffff0000, v121
	v_lshlrev_b32_e32 v122, 16, v123
	v_and_b32_e32 v123, 0xffff0000, v123
	v_lshl_add_u64 v[118:119], s[8:9], 0, v[118:119]
	v_addc_co_u32_e32 v129, vcc, 0, v127, vcc
	v_pk_fma_f32 v[116:117], v[116:117], v[120:121], v[122:123]
	v_lshl_add_u64 v[118:119], v[118:119], 0, v[142:143]
	v_cvt_pk_bf16_f32 v114, v114, v115
	v_cvt_pk_bf16_f32 v115, v116, v117
	v_mov_b32_e32 v116, v184
	v_mov_b32_e32 v117, v185
	v_mov_b32_e32 v120, v186
	v_mov_b32_e32 v121, v187
	v_lshl_add_u64 v[122:123], v[126:127], 0, s[10:11]
	global_store_dwordx2 v[160:161], v[114:115], off offset:288
	s_nop 0
	v_lshlrev_b32_e32 v114, 16, v116
	v_and_b32_e32 v115, 0xffff0000, v116
	v_lshlrev_b32_e32 v116, 16, v117
	v_and_b32_e32 v117, 0xffff0000, v117
	v_lshlrev_b32_e32 v124, 16, v120
	v_and_b32_e32 v125, 0xffff0000, v120
	v_lshlrev_b32_e32 v120, 16, v121
	v_and_b32_e32 v121, 0xffff0000, v121
	v_pk_fma_f32 v[112:113], v[112:113], v[116:117], v[120:121]
	v_pk_fma_f32 v[110:111], v[110:111], v[114:115], v[124:125]
	s_nop 0
	v_cvt_pk_bf16_f32 v110, v110, v111
	v_cvt_pk_bf16_f32 v111, v112, v113
	v_mov_b32_e32 v112, v192
	v_mov_b32_e32 v113, v193
	v_mov_b32_e32 v114, v194
	v_mov_b32_e32 v115, v195
	s_nop 0
	v_lshlrev_b32_e32 v116, 16, v114
	global_store_dwordx2 v[118:119], v[110:111], off
	v_lshlrev_b32_e32 v110, 16, v112
	v_and_b32_e32 v111, 0xffff0000, v112
	v_lshlrev_b32_e32 v112, 16, v113
	v_and_b32_e32 v113, 0xffff0000, v113
	v_and_b32_e32 v117, 0xffff0000, v114
	v_lshlrev_b32_e32 v114, 16, v115
	v_and_b32_e32 v115, 0xffff0000, v115
	v_pk_fma_f32 v[108:109], v[108:109], v[112:113], v[114:115]
	v_pk_fma_f32 v[106:107], v[106:107], v[110:111], v[116:117]
	s_nop 0
	v_cvt_pk_bf16_f32 v106, v106, v107
	v_cvt_pk_bf16_f32 v107, v108, v109
	v_mov_b32_e32 v108, v196
	v_mov_b32_e32 v109, v197
	v_mov_b32_e32 v110, v198
	v_mov_b32_e32 v111, v199
	s_nop 0
	v_lshlrev_b32_e32 v112, 16, v110
	global_store_dwordx2 v[118:119], v[106:107], off offset:32
	v_lshlrev_b32_e32 v106, 16, v108
	v_and_b32_e32 v107, 0xffff0000, v108
	v_lshlrev_b32_e32 v108, 16, v109
	v_and_b32_e32 v109, 0xffff0000, v109
	v_and_b32_e32 v113, 0xffff0000, v110
	v_lshlrev_b32_e32 v110, 16, v111
	v_and_b32_e32 v111, 0xffff0000, v111
	v_pk_fma_f32 v[104:105], v[104:105], v[108:109], v[110:111]
	v_pk_fma_f32 v[102:103], v[102:103], v[106:107], v[112:113]
	v_or_b32_e32 v108, 32, v144
	v_cvt_pk_bf16_f32 v102, v102, v103
	v_cvt_pk_bf16_f32 v103, v104, v105
	v_mov_b32_e32 v104, v200
	v_mov_b32_e32 v105, v201
	v_mov_b32_e32 v106, v202
	v_mov_b32_e32 v107, v203
	v_ashrrev_i32_e32 v109, 31, v108
	v_mad_i64_i32 v[110:111], s[22:23], v108, s48, v[146:147]
	global_store_dwordx2 v[118:119], v[102:103], off offset:256
	v_lshl_add_u64 v[110:111], v[110:111], 0, v[142:143]
	v_add_co_u32_e32 v112, vcc, s49, v110
	s_nop 0
	v_lshlrev_b32_e32 v102, 16, v104
	v_and_b32_e32 v103, 0xffff0000, v104
	v_lshlrev_b32_e32 v114, 16, v106
	v_and_b32_e32 v115, 0xffff0000, v106
	v_pk_fma_f32 v[98:99], v[98:99], v[102:103], v[114:115]
	v_lshlrev_b64 v[102:103], 12, v[108:109]
	v_lshlrev_b32_e32 v104, 16, v105
	v_and_b32_e32 v105, 0xffff0000, v105
	v_lshlrev_b32_e32 v106, 16, v107
	v_and_b32_e32 v107, 0xffff0000, v107
	v_lshl_add_u64 v[102:103], s[8:9], 0, v[102:103]
	v_addc_co_u32_e32 v113, vcc, 0, v111, vcc
	v_pk_fma_f32 v[100:101], v[100:101], v[104:105], v[106:107]
	v_lshl_add_u64 v[102:103], v[102:103], 0, v[142:143]
	v_cvt_pk_bf16_f32 v98, v98, v99
	v_cvt_pk_bf16_f32 v99, v100, v101
	v_mov_b32_e32 v100, v204
	v_mov_b32_e32 v101, v205
	v_mov_b32_e32 v104, v206
	v_mov_b32_e32 v105, v207
	v_lshl_add_u64 v[106:107], v[110:111], 0, s[10:11]
	global_store_dwordx2 v[118:119], v[98:99], off offset:288
	s_nop 0
	v_lshlrev_b32_e32 v98, 16, v100
	v_and_b32_e32 v99, 0xffff0000, v100
	v_lshlrev_b32_e32 v100, 16, v101
	v_and_b32_e32 v101, 0xffff0000, v101
	v_lshlrev_b32_e32 v108, 16, v104
	v_and_b32_e32 v109, 0xffff0000, v104
	v_lshlrev_b32_e32 v104, 16, v105
	v_and_b32_e32 v105, 0xffff0000, v105
	v_pk_fma_f32 v[96:97], v[96:97], v[100:101], v[104:105]
	v_pk_fma_f32 v[94:95], v[94:95], v[98:99], v[108:109]
	s_nop 0
	v_cvt_pk_bf16_f32 v94, v94, v95
	v_cvt_pk_bf16_f32 v95, v96, v97
	v_mov_b32_e32 v96, v208
	v_mov_b32_e32 v97, v209
	v_mov_b32_e32 v98, v210
	v_mov_b32_e32 v99, v211
	s_nop 0
	v_lshlrev_b32_e32 v100, 16, v98
	global_store_dwordx2 v[102:103], v[94:95], off
	v_lshlrev_b32_e32 v94, 16, v96
	v_and_b32_e32 v95, 0xffff0000, v96
	v_lshlrev_b32_e32 v96, 16, v97
	v_and_b32_e32 v97, 0xffff0000, v97
	v_and_b32_e32 v101, 0xffff0000, v98
	v_lshlrev_b32_e32 v98, 16, v99
	v_and_b32_e32 v99, 0xffff0000, v99
	v_pk_fma_f32 v[92:93], v[92:93], v[96:97], v[98:99]
	v_pk_fma_f32 v[90:91], v[90:91], v[94:95], v[100:101]
	s_nop 0
	v_cvt_pk_bf16_f32 v90, v90, v91
	v_cvt_pk_bf16_f32 v91, v92, v93
	v_mov_b32_e32 v92, v212
	v_mov_b32_e32 v93, v213
	v_mov_b32_e32 v94, v214
	v_mov_b32_e32 v95, v215
	s_nop 0
	v_lshlrev_b32_e32 v96, 16, v94
	global_store_dwordx2 v[102:103], v[90:91], off offset:32
	v_lshlrev_b32_e32 v90, 16, v92
	v_and_b32_e32 v91, 0xffff0000, v92
	v_lshlrev_b32_e32 v92, 16, v93
	v_and_b32_e32 v93, 0xffff0000, v93
	v_and_b32_e32 v97, 0xffff0000, v94
	v_lshlrev_b32_e32 v94, 16, v95
	v_and_b32_e32 v95, 0xffff0000, v95
	v_pk_fma_f32 v[88:89], v[88:89], v[92:93], v[94:95]
	v_pk_fma_f32 v[86:87], v[86:87], v[90:91], v[96:97]
	v_or_b32_e32 v92, 48, v144
	v_cvt_pk_bf16_f32 v86, v86, v87
	v_cvt_pk_bf16_f32 v87, v88, v89
	v_mov_b32_e32 v88, v216
	v_mov_b32_e32 v89, v217
	v_mov_b32_e32 v90, v218
	v_mov_b32_e32 v91, v219
	v_ashrrev_i32_e32 v93, 31, v92
	v_mad_i64_i32 v[94:95], s[22:23], v92, s48, v[146:147]
	global_store_dwordx2 v[102:103], v[86:87], off offset:256
	v_lshl_add_u64 v[94:95], v[94:95], 0, v[142:143]
	v_add_co_u32_e32 v96, vcc, s49, v94
	s_nop 0
	v_lshlrev_b32_e32 v86, 16, v88
	v_and_b32_e32 v87, 0xffff0000, v88
	v_lshlrev_b32_e32 v98, 16, v90
	v_and_b32_e32 v99, 0xffff0000, v90
	v_pk_fma_f32 v[82:83], v[82:83], v[86:87], v[98:99]
	v_lshlrev_b64 v[86:87], 12, v[92:93]
	v_lshlrev_b32_e32 v88, 16, v89
	v_and_b32_e32 v89, 0xffff0000, v89
	v_lshlrev_b32_e32 v90, 16, v91
	v_and_b32_e32 v91, 0xffff0000, v91
	v_lshl_add_u64 v[86:87], s[8:9], 0, v[86:87]
	v_addc_co_u32_e32 v97, vcc, 0, v95, vcc
	v_pk_fma_f32 v[84:85], v[84:85], v[88:89], v[90:91]
	v_lshl_add_u64 v[86:87], v[86:87], 0, v[142:143]
	v_cvt_pk_bf16_f32 v82, v82, v83
	v_cvt_pk_bf16_f32 v83, v84, v85
	v_mov_b32_e32 v237, 0x1000
	v_mov_b32_e32 v236, 48
	v_mad_i64_i32 v[230:231], s[22:23], v236, s48, v[228:229]
	v_mad_i64_i32 v[234:235], s[22:23], v236, v237, v[232:233]
	global_load_dwordx2 v[168:169], v[230:231], off
	global_load_dwordx2 v[170:171], v[234:235], off
	global_load_dwordx2 v[172:173], v[230:231], off offset:32
	global_load_dwordx2 v[174:175], v[234:235], off offset:32
	global_load_dwordx2 v[176:177], v[230:231], off offset:256
	global_load_dwordx2 v[178:179], v[234:235], off offset:256
	global_load_dwordx2 v[180:181], v[230:231], off offset:288
	global_load_dwordx2 v[182:183], v[234:235], off offset:288
	v_mov_b32_e32 v236, 128
	v_mad_i64_i32 v[230:231], s[22:23], v236, s48, v[228:229]
	v_mad_i64_i32 v[234:235], s[22:23], v236, v237, v[232:233]
	global_load_dwordx2 v[184:185], v[230:231], off
	global_load_dwordx2 v[186:187], v[234:235], off
	global_load_dwordx2 v[192:193], v[230:231], off offset:32
	global_load_dwordx2 v[194:195], v[234:235], off offset:32
	global_load_dwordx2 v[196:197], v[230:231], off offset:256
	global_load_dwordx2 v[198:199], v[234:235], off offset:256
	global_load_dwordx2 v[200:201], v[230:231], off offset:288
	global_load_dwordx2 v[202:203], v[234:235], off offset:288
	v_mov_b32_e32 v236, 144
	v_mad_i64_i32 v[230:231], s[22:23], v236, s48, v[228:229]
	v_mad_i64_i32 v[234:235], s[22:23], v236, v237, v[232:233]
	global_load_dwordx2 v[204:205], v[230:231], off
	global_load_dwordx2 v[206:207], v[234:235], off
	global_load_dwordx2 v[208:209], v[230:231], off offset:32
	global_load_dwordx2 v[210:211], v[234:235], off offset:32
	global_load_dwordx2 v[212:213], v[230:231], off offset:256
	global_load_dwordx2 v[214:215], v[234:235], off offset:256
	global_load_dwordx2 v[216:217], v[230:231], off offset:288
	global_load_dwordx2 v[218:219], v[234:235], off offset:288
	s_waitcnt vmcnt(0)
	v_mov_b32_e32 v84, v168
	v_mov_b32_e32 v85, v169
	v_mov_b32_e32 v88, v170
	v_mov_b32_e32 v89, v171
	v_lshl_add_u64 v[90:91], v[94:95], 0, s[10:11]
	global_store_dwordx2 v[102:103], v[82:83], off offset:288
	s_nop 0
	v_lshlrev_b32_e32 v82, 16, v84
	v_and_b32_e32 v83, 0xffff0000, v84
	v_lshlrev_b32_e32 v84, 16, v85
	v_and_b32_e32 v85, 0xffff0000, v85
	v_lshlrev_b32_e32 v92, 16, v88
	v_and_b32_e32 v93, 0xffff0000, v88
	v_lshlrev_b32_e32 v88, 16, v89
	v_and_b32_e32 v89, 0xffff0000, v89
	v_pk_fma_f32 v[80:81], v[80:81], v[84:85], v[88:89]
	v_pk_fma_f32 v[78:79], v[78:79], v[82:83], v[92:93]
	s_nop 0
	v_cvt_pk_bf16_f32 v78, v78, v79
	v_cvt_pk_bf16_f32 v79, v80, v81
	v_mov_b32_e32 v80, v172
	v_mov_b32_e32 v81, v173
	v_mov_b32_e32 v82, v174
	v_mov_b32_e32 v83, v175
	s_nop 0
	v_lshlrev_b32_e32 v84, 16, v82
	global_store_dwordx2 v[86:87], v[78:79], off
	v_lshlrev_b32_e32 v78, 16, v80
	v_and_b32_e32 v79, 0xffff0000, v80
	v_lshlrev_b32_e32 v80, 16, v81
	v_and_b32_e32 v81, 0xffff0000, v81
	v_and_b32_e32 v85, 0xffff0000, v82
	v_lshlrev_b32_e32 v82, 16, v83
	v_and_b32_e32 v83, 0xffff0000, v83
	v_pk_fma_f32 v[76:77], v[76:77], v[80:81], v[82:83]
	v_pk_fma_f32 v[74:75], v[74:75], v[78:79], v[84:85]
	s_nop 0
	v_cvt_pk_bf16_f32 v74, v74, v75
	v_cvt_pk_bf16_f32 v75, v76, v77
	v_mov_b32_e32 v76, v176
	v_mov_b32_e32 v77, v177
	v_mov_b32_e32 v78, v178
	v_mov_b32_e32 v79, v179
	s_nop 0
	v_lshlrev_b32_e32 v80, 16, v78
	global_store_dwordx2 v[86:87], v[74:75], off offset:32
	v_lshlrev_b32_e32 v74, 16, v76
	v_and_b32_e32 v75, 0xffff0000, v76
	v_lshlrev_b32_e32 v76, 16, v77
	v_and_b32_e32 v77, 0xffff0000, v77
	v_and_b32_e32 v81, 0xffff0000, v78
	v_lshlrev_b32_e32 v78, 16, v79
	v_and_b32_e32 v79, 0xffff0000, v79
	v_pk_fma_f32 v[72:73], v[72:73], v[76:77], v[78:79]
	v_pk_fma_f32 v[70:71], v[70:71], v[74:75], v[80:81]
	v_add_u32_e32 v76, 0x80, v144
	v_cvt_pk_bf16_f32 v70, v70, v71
	v_cvt_pk_bf16_f32 v71, v72, v73
	v_mov_b32_e32 v72, v180
	v_mov_b32_e32 v73, v181
	v_mov_b32_e32 v74, v182
	v_mov_b32_e32 v75, v183
	v_ashrrev_i32_e32 v77, 31, v76
	v_mad_i64_i32 v[78:79], s[22:23], v76, s48, v[146:147]
	global_store_dwordx2 v[86:87], v[70:71], off offset:256
	v_lshl_add_u64 v[78:79], v[78:79], 0, v[142:143]
	v_add_co_u32_e32 v80, vcc, s49, v78
	s_nop 0
	v_lshlrev_b32_e32 v70, 16, v72
	v_and_b32_e32 v71, 0xffff0000, v72
	v_lshlrev_b32_e32 v82, 16, v74
	v_and_b32_e32 v83, 0xffff0000, v74
	v_pk_fma_f32 v[66:67], v[66:67], v[70:71], v[82:83]
	v_lshlrev_b64 v[70:71], 12, v[76:77]
	v_lshlrev_b32_e32 v72, 16, v73
	v_and_b32_e32 v73, 0xffff0000, v73
	v_lshlrev_b32_e32 v74, 16, v75
	v_and_b32_e32 v75, 0xffff0000, v75
	v_lshl_add_u64 v[70:71], s[8:9], 0, v[70:71]
	v_addc_co_u32_e32 v81, vcc, 0, v79, vcc
	v_pk_fma_f32 v[68:69], v[68:69], v[72:73], v[74:75]
	v_lshl_add_u64 v[70:71], v[70:71], 0, v[142:143]
	v_cvt_pk_bf16_f32 v66, v66, v67
	v_cvt_pk_bf16_f32 v67, v68, v69
	v_mov_b32_e32 v68, v184
	v_mov_b32_e32 v69, v185
	v_mov_b32_e32 v72, v186
	v_mov_b32_e32 v73, v187
	v_lshl_add_u64 v[74:75], v[78:79], 0, s[10:11]
	global_store_dwordx2 v[86:87], v[66:67], off offset:288
	s_nop 0
	v_lshlrev_b32_e32 v66, 16, v68
	v_and_b32_e32 v67, 0xffff0000, v68
	v_lshlrev_b32_e32 v68, 16, v69
	v_and_b32_e32 v69, 0xffff0000, v69
	v_lshlrev_b32_e32 v76, 16, v72
	v_and_b32_e32 v77, 0xffff0000, v72
	v_lshlrev_b32_e32 v72, 16, v73
	v_and_b32_e32 v73, 0xffff0000, v73
	v_pk_fma_f32 v[64:65], v[64:65], v[68:69], v[72:73]
	v_pk_fma_f32 v[62:63], v[62:63], v[66:67], v[76:77]
	s_nop 0
	v_cvt_pk_bf16_f32 v62, v62, v63
	v_cvt_pk_bf16_f32 v63, v64, v65
	v_mov_b32_e32 v64, v192
	v_mov_b32_e32 v65, v193
	v_mov_b32_e32 v66, v194
	v_mov_b32_e32 v67, v195
	s_nop 0
	v_lshlrev_b32_e32 v68, 16, v66
	global_store_dwordx2 v[70:71], v[62:63], off
	v_lshlrev_b32_e32 v62, 16, v64
	v_and_b32_e32 v63, 0xffff0000, v64
	v_lshlrev_b32_e32 v64, 16, v65
	v_and_b32_e32 v65, 0xffff0000, v65
	v_and_b32_e32 v69, 0xffff0000, v66
	v_lshlrev_b32_e32 v66, 16, v67
	v_and_b32_e32 v67, 0xffff0000, v67
	v_pk_fma_f32 v[60:61], v[60:61], v[64:65], v[66:67]
	v_pk_fma_f32 v[58:59], v[58:59], v[62:63], v[68:69]
	s_nop 0
	v_cvt_pk_bf16_f32 v58, v58, v59
	v_cvt_pk_bf16_f32 v59, v60, v61
	v_mov_b32_e32 v60, v196
	v_mov_b32_e32 v61, v197
	v_mov_b32_e32 v62, v198
	v_mov_b32_e32 v63, v199
	s_nop 0
	v_lshlrev_b32_e32 v64, 16, v62
	global_store_dwordx2 v[70:71], v[58:59], off offset:32
	v_lshlrev_b32_e32 v58, 16, v60
	v_and_b32_e32 v59, 0xffff0000, v60
	v_lshlrev_b32_e32 v60, 16, v61
	v_and_b32_e32 v61, 0xffff0000, v61
	v_and_b32_e32 v65, 0xffff0000, v62
	v_lshlrev_b32_e32 v62, 16, v63
	v_and_b32_e32 v63, 0xffff0000, v63
	v_pk_fma_f32 v[56:57], v[56:57], v[60:61], v[62:63]
	v_pk_fma_f32 v[54:55], v[54:55], v[58:59], v[64:65]
	v_add_u32_e32 v60, 0x90, v144
	v_cvt_pk_bf16_f32 v54, v54, v55
	v_cvt_pk_bf16_f32 v55, v56, v57
	v_mov_b32_e32 v56, v200
	v_mov_b32_e32 v57, v201
	v_mov_b32_e32 v58, v202
	v_mov_b32_e32 v59, v203
	v_ashrrev_i32_e32 v61, 31, v60
	v_mad_i64_i32 v[62:63], s[22:23], v60, s48, v[146:147]
	global_store_dwordx2 v[70:71], v[54:55], off offset:256
	v_lshl_add_u64 v[62:63], v[62:63], 0, v[142:143]
	v_add_co_u32_e32 v64, vcc, s49, v62
	s_nop 0
	v_lshlrev_b32_e32 v54, 16, v56
	v_and_b32_e32 v55, 0xffff0000, v56
	v_lshlrev_b32_e32 v66, 16, v58
	v_and_b32_e32 v67, 0xffff0000, v58
	v_pk_fma_f32 v[50:51], v[50:51], v[54:55], v[66:67]
	v_lshlrev_b64 v[54:55], 12, v[60:61]
	v_lshlrev_b32_e32 v56, 16, v57
	v_and_b32_e32 v57, 0xffff0000, v57
	v_lshlrev_b32_e32 v58, 16, v59
	v_and_b32_e32 v59, 0xffff0000, v59
	v_lshl_add_u64 v[54:55], s[8:9], 0, v[54:55]
	v_addc_co_u32_e32 v65, vcc, 0, v63, vcc
	v_pk_fma_f32 v[52:53], v[52:53], v[56:57], v[58:59]
	v_lshl_add_u64 v[54:55], v[54:55], 0, v[142:143]
	v_cvt_pk_bf16_f32 v50, v50, v51
	v_cvt_pk_bf16_f32 v51, v52, v53
	v_mov_b32_e32 v52, v204
	v_mov_b32_e32 v53, v205
	v_mov_b32_e32 v56, v206
	v_mov_b32_e32 v57, v207
	v_lshl_add_u64 v[58:59], v[62:63], 0, s[10:11]
	global_store_dwordx2 v[70:71], v[50:51], off offset:288
	s_nop 0
	v_lshlrev_b32_e32 v50, 16, v52
	v_and_b32_e32 v51, 0xffff0000, v52
	v_lshlrev_b32_e32 v52, 16, v53
	v_and_b32_e32 v53, 0xffff0000, v53
	v_lshlrev_b32_e32 v60, 16, v56
	v_and_b32_e32 v61, 0xffff0000, v56
	v_lshlrev_b32_e32 v56, 16, v57
	v_and_b32_e32 v57, 0xffff0000, v57
	v_pk_fma_f32 v[48:49], v[48:49], v[52:53], v[56:57]
	v_pk_fma_f32 v[46:47], v[46:47], v[50:51], v[60:61]
	s_nop 0
	v_cvt_pk_bf16_f32 v46, v46, v47
	v_cvt_pk_bf16_f32 v47, v48, v49
	v_mov_b32_e32 v48, v208
	v_mov_b32_e32 v49, v209
	v_mov_b32_e32 v50, v210
	v_mov_b32_e32 v51, v211
	s_nop 0
	v_lshlrev_b32_e32 v52, 16, v50
	global_store_dwordx2 v[54:55], v[46:47], off
	v_lshlrev_b32_e32 v46, 16, v48
	v_and_b32_e32 v47, 0xffff0000, v48
	v_lshlrev_b32_e32 v48, 16, v49
	v_and_b32_e32 v49, 0xffff0000, v49
	v_and_b32_e32 v53, 0xffff0000, v50
	v_lshlrev_b32_e32 v50, 16, v51
	v_and_b32_e32 v51, 0xffff0000, v51
	v_pk_fma_f32 v[44:45], v[44:45], v[48:49], v[50:51]
	v_pk_fma_f32 v[42:43], v[42:43], v[46:47], v[52:53]
	s_nop 0
	v_cvt_pk_bf16_f32 v42, v42, v43
	v_cvt_pk_bf16_f32 v43, v44, v45
	v_mov_b32_e32 v44, v212
	v_mov_b32_e32 v45, v213
	v_mov_b32_e32 v46, v214
	v_mov_b32_e32 v47, v215
	s_nop 0
	v_lshlrev_b32_e32 v48, 16, v46
	global_store_dwordx2 v[54:55], v[42:43], off offset:32
	v_lshlrev_b32_e32 v42, 16, v44
	v_and_b32_e32 v43, 0xffff0000, v44
	v_lshlrev_b32_e32 v44, 16, v45
	v_and_b32_e32 v45, 0xffff0000, v45
	v_and_b32_e32 v49, 0xffff0000, v46
	v_lshlrev_b32_e32 v46, 16, v47
	v_and_b32_e32 v47, 0xffff0000, v47
	v_pk_fma_f32 v[40:41], v[40:41], v[44:45], v[46:47]
	v_pk_fma_f32 v[38:39], v[38:39], v[42:43], v[48:49]
	v_add_u32_e32 v44, 0xa0, v144
	v_cvt_pk_bf16_f32 v38, v38, v39
	v_cvt_pk_bf16_f32 v39, v40, v41
	v_mov_b32_e32 v40, v216
	v_mov_b32_e32 v41, v217
	v_mov_b32_e32 v42, v218
	v_mov_b32_e32 v43, v219
	v_ashrrev_i32_e32 v45, 31, v44
	v_mad_i64_i32 v[46:47], s[22:23], v44, s48, v[146:147]
	global_store_dwordx2 v[54:55], v[38:39], off offset:256
	v_lshl_add_u64 v[46:47], v[46:47], 0, v[142:143]
	v_add_co_u32_e32 v48, vcc, s49, v46
	s_nop 0
	v_lshlrev_b32_e32 v38, 16, v40
	v_and_b32_e32 v39, 0xffff0000, v40
	v_lshlrev_b32_e32 v50, 16, v42
	v_and_b32_e32 v51, 0xffff0000, v42
	v_pk_fma_f32 v[34:35], v[34:35], v[38:39], v[50:51]
	v_lshlrev_b64 v[38:39], 12, v[44:45]
	v_lshlrev_b32_e32 v40, 16, v41
	v_and_b32_e32 v41, 0xffff0000, v41
	v_lshlrev_b32_e32 v42, 16, v43
	v_and_b32_e32 v43, 0xffff0000, v43
	v_lshl_add_u64 v[38:39], s[8:9], 0, v[38:39]
	v_addc_co_u32_e32 v49, vcc, 0, v47, vcc
	v_pk_fma_f32 v[36:37], v[36:37], v[40:41], v[42:43]
	v_lshl_add_u64 v[38:39], v[38:39], 0, v[142:143]
	v_cvt_pk_bf16_f32 v34, v34, v35
	v_cvt_pk_bf16_f32 v35, v36, v37
	v_mov_b32_e32 v237, 0x1000
	v_mov_b32_e32 v236, 160
	v_mad_i64_i32 v[230:231], s[22:23], v236, s48, v[228:229]
	v_mad_i64_i32 v[234:235], s[22:23], v236, v237, v[232:233]
	global_load_dwordx2 v[168:169], v[230:231], off
	global_load_dwordx2 v[170:171], v[234:235], off
	global_load_dwordx2 v[172:173], v[230:231], off offset:32
	global_load_dwordx2 v[174:175], v[234:235], off offset:32
	global_load_dwordx2 v[176:177], v[230:231], off offset:256
	global_load_dwordx2 v[178:179], v[234:235], off offset:256
	global_load_dwordx2 v[180:181], v[230:231], off offset:288
	global_load_dwordx2 v[182:183], v[234:235], off offset:288
	v_mov_b32_e32 v236, 176
	v_mad_i64_i32 v[230:231], s[22:23], v236, s48, v[228:229]
	v_mad_i64_i32 v[234:235], s[22:23], v236, v237, v[232:233]
	global_load_dwordx2 v[184:185], v[230:231], off
	global_load_dwordx2 v[186:187], v[234:235], off
	global_load_dwordx2 v[192:193], v[230:231], off offset:32
	global_load_dwordx2 v[194:195], v[234:235], off offset:32
	global_load_dwordx2 v[196:197], v[230:231], off offset:256
	global_load_dwordx2 v[198:199], v[234:235], off offset:256
	global_load_dwordx2 v[200:201], v[230:231], off offset:288
	global_load_dwordx2 v[202:203], v[234:235], off offset:288
	s_waitcnt vmcnt(0)
	v_mov_b32_e32 v36, v168
	v_mov_b32_e32 v37, v169
	v_mov_b32_e32 v40, v170
	v_mov_b32_e32 v41, v171
	v_lshl_add_u64 v[42:43], v[46:47], 0, s[10:11]
	global_store_dwordx2 v[54:55], v[34:35], off offset:288
	s_nop 0
	v_lshlrev_b32_e32 v34, 16, v36
	v_and_b32_e32 v35, 0xffff0000, v36
	v_lshlrev_b32_e32 v36, 16, v37
	v_and_b32_e32 v37, 0xffff0000, v37
	v_lshlrev_b32_e32 v44, 16, v40
	v_and_b32_e32 v45, 0xffff0000, v40
	v_lshlrev_b32_e32 v40, 16, v41
	v_and_b32_e32 v41, 0xffff0000, v41
	v_pk_fma_f32 v[32:33], v[32:33], v[36:37], v[40:41]
	v_pk_fma_f32 v[30:31], v[30:31], v[34:35], v[44:45]
	s_nop 0
	v_cvt_pk_bf16_f32 v30, v30, v31
	v_cvt_pk_bf16_f32 v31, v32, v33
	v_mov_b32_e32 v32, v172
	v_mov_b32_e32 v33, v173
	v_mov_b32_e32 v34, v174
	v_mov_b32_e32 v35, v175
	s_nop 0
	v_lshlrev_b32_e32 v36, 16, v34
	global_store_dwordx2 v[38:39], v[30:31], off
	v_lshlrev_b32_e32 v30, 16, v32
	v_and_b32_e32 v31, 0xffff0000, v32
	v_lshlrev_b32_e32 v32, 16, v33
	v_and_b32_e32 v33, 0xffff0000, v33
	v_and_b32_e32 v37, 0xffff0000, v34
	v_lshlrev_b32_e32 v34, 16, v35
	v_and_b32_e32 v35, 0xffff0000, v35
	v_pk_fma_f32 v[28:29], v[28:29], v[32:33], v[34:35]
	v_pk_fma_f32 v[26:27], v[26:27], v[30:31], v[36:37]
	s_nop 0
	v_cvt_pk_bf16_f32 v26, v26, v27
	v_cvt_pk_bf16_f32 v27, v28, v29
	v_mov_b32_e32 v28, v176
	v_mov_b32_e32 v29, v177
	v_mov_b32_e32 v30, v178
	v_mov_b32_e32 v31, v179
	s_nop 0
	v_lshlrev_b32_e32 v32, 16, v30
	global_store_dwordx2 v[38:39], v[26:27], off offset:32
	v_lshlrev_b32_e32 v26, 16, v28
	v_and_b32_e32 v27, 0xffff0000, v28
	v_lshlrev_b32_e32 v28, 16, v29
	v_and_b32_e32 v29, 0xffff0000, v29
	v_and_b32_e32 v33, 0xffff0000, v30
	v_lshlrev_b32_e32 v30, 16, v31
	v_and_b32_e32 v31, 0xffff0000, v31
	v_pk_fma_f32 v[24:25], v[24:25], v[28:29], v[30:31]
	v_pk_fma_f32 v[22:23], v[22:23], v[26:27], v[32:33]
	v_add_u32_e32 v28, 0xb0, v144
	v_cvt_pk_bf16_f32 v22, v22, v23
	v_cvt_pk_bf16_f32 v23, v24, v25
	v_mov_b32_e32 v24, v180
	v_mov_b32_e32 v25, v181
	v_mov_b32_e32 v26, v182
	v_mov_b32_e32 v27, v183
	v_ashrrev_i32_e32 v29, 31, v28
	v_mad_i64_i32 v[30:31], s[22:23], v28, s48, v[146:147]
	global_store_dwordx2 v[38:39], v[22:23], off offset:256
	v_lshl_add_u64 v[30:31], v[30:31], 0, v[142:143]
	v_add_co_u32_e32 v32, vcc, s49, v30
	s_mov_b64 s[22:23], s[16:17]
	s_nop 0
	v_addc_co_u32_e32 v33, vcc, 0, v31, vcc
	s_and_b64 vcc, exec, s[0:1]
	s_nop 0
	v_lshlrev_b32_e32 v22, 16, v24
	v_and_b32_e32 v23, 0xffff0000, v24
	v_lshlrev_b32_e32 v34, 16, v26
	v_and_b32_e32 v35, 0xffff0000, v26
	v_pk_fma_f32 v[18:19], v[18:19], v[22:23], v[34:35]
	v_lshlrev_b64 v[22:23], 12, v[28:29]
	v_lshlrev_b32_e32 v24, 16, v25
	v_and_b32_e32 v25, 0xffff0000, v25
	v_lshlrev_b32_e32 v26, 16, v27
	v_and_b32_e32 v27, 0xffff0000, v27
	v_lshl_add_u64 v[22:23], s[8:9], 0, v[22:23]
	v_pk_fma_f32 v[20:21], v[20:21], v[24:25], v[26:27]
	v_lshl_add_u64 v[22:23], v[22:23], 0, v[142:143]
	v_cvt_pk_bf16_f32 v18, v18, v19
	v_cvt_pk_bf16_f32 v19, v20, v21
	v_mov_b32_e32 v20, v184
	v_mov_b32_e32 v21, v185
	v_mov_b32_e32 v24, v186
	v_mov_b32_e32 v25, v187
	v_lshl_add_u64 v[26:27], v[30:31], 0, s[10:11]
	global_store_dwordx2 v[38:39], v[18:19], off offset:288
	s_nop 0
	v_lshlrev_b32_e32 v18, 16, v20
	v_and_b32_e32 v19, 0xffff0000, v20
	v_lshlrev_b32_e32 v20, 16, v21
	v_and_b32_e32 v21, 0xffff0000, v21
	v_lshlrev_b32_e32 v28, 16, v24
	v_and_b32_e32 v29, 0xffff0000, v24
	v_lshlrev_b32_e32 v24, 16, v25
	v_and_b32_e32 v25, 0xffff0000, v25
	v_pk_fma_f32 v[16:17], v[16:17], v[20:21], v[24:25]
	v_pk_fma_f32 v[14:15], v[14:15], v[18:19], v[28:29]
	s_nop 0
	v_cvt_pk_bf16_f32 v14, v14, v15
	v_cvt_pk_bf16_f32 v15, v16, v17
	v_mov_b32_e32 v16, v192
	v_mov_b32_e32 v17, v193
	v_mov_b32_e32 v18, v194
	v_mov_b32_e32 v19, v195
	s_nop 0
	v_lshlrev_b32_e32 v20, 16, v18
	global_store_dwordx2 v[22:23], v[14:15], off
	v_lshlrev_b32_e32 v14, 16, v16
	v_and_b32_e32 v15, 0xffff0000, v16
	v_lshlrev_b32_e32 v16, 16, v17
	v_and_b32_e32 v17, 0xffff0000, v17
	v_and_b32_e32 v21, 0xffff0000, v18
	v_lshlrev_b32_e32 v18, 16, v19
	v_and_b32_e32 v19, 0xffff0000, v19
	v_pk_fma_f32 v[12:13], v[12:13], v[16:17], v[18:19]
	v_pk_fma_f32 v[10:11], v[10:11], v[14:15], v[20:21]
	s_nop 0
	v_cvt_pk_bf16_f32 v10, v10, v11
	v_cvt_pk_bf16_f32 v11, v12, v13
	v_mov_b32_e32 v12, v196
	v_mov_b32_e32 v13, v197
	v_mov_b32_e32 v14, v198
	v_mov_b32_e32 v15, v199
	s_nop 0
	v_lshlrev_b32_e32 v16, 16, v14
	global_store_dwordx2 v[22:23], v[10:11], off offset:32
	v_lshlrev_b32_e32 v10, 16, v12
	v_and_b32_e32 v11, 0xffff0000, v12
	v_lshlrev_b32_e32 v12, 16, v13
	v_and_b32_e32 v13, 0xffff0000, v13
	v_and_b32_e32 v17, 0xffff0000, v14
	v_lshlrev_b32_e32 v14, 16, v15
	v_and_b32_e32 v15, 0xffff0000, v15
	v_pk_fma_f32 v[8:9], v[8:9], v[12:13], v[14:15]
	v_pk_fma_f32 v[6:7], v[6:7], v[10:11], v[16:17]
	s_nop 0
	v_cvt_pk_bf16_f32 v6, v6, v7
	v_cvt_pk_bf16_f32 v7, v8, v9
	v_mov_b32_e32 v8, v200
	v_mov_b32_e32 v9, v201
	v_mov_b32_e32 v10, v202
	v_mov_b32_e32 v11, v203
	s_nop 0
	v_lshlrev_b32_e32 v12, 16, v10
	global_store_dwordx2 v[22:23], v[6:7], off offset:256
	v_lshlrev_b32_e32 v6, 16, v8
	v_and_b32_e32 v7, 0xffff0000, v8
	v_and_b32_e32 v13, 0xffff0000, v10
	v_lshlrev_b32_e32 v8, 16, v9
	v_and_b32_e32 v9, 0xffff0000, v9
	v_lshlrev_b32_e32 v10, 16, v11
	v_and_b32_e32 v11, 0xffff0000, v11
	v_pk_fma_f32 v[2:3], v[2:3], v[6:7], v[12:13]
	v_pk_fma_f32 v[4:5], v[4:5], v[8:9], v[10:11]
	v_cvt_pk_bf16_f32 v2, v2, v3
	s_nop 0
	v_cvt_pk_bf16_f32 v3, v4, v5
	global_store_dwordx2 v[22:23], v[2:3], off offset:288
	s_cbranch_vccz .LBB0_1220
	s_waitcnt vmcnt(0)
	s_cmpk_gt_u32 s28, 0xff
	s_cbranch_scc1 .LBB0_1227
	s_barrier

.LBB0_2730:
	s_or_b64 exec, exec, s[0:1]
	s_add_i32 s0, 0, 0x21000
	v_mov_b32_e32 v2, s0
	v_readlane_b32 s0, v251, 26
	v_mov_b32_e32 v92, v174
	v_mov_b32_e32 v22, v180
	s_waitcnt lgkmcnt(0)
	v_mov_b32_e32 v3, s0
	v_mov_b32_e32 v23, v181
	v_mov_b32_e32 v10, v164
	s_barrier
	ds_read_b128 v[6:9], v2
	ds_read_b128 v[2:5], v3
	v_mov_b32_e32 v60, v165
	v_mov_b32_e32 v34, v166
	v_mov_b32_e32 v62, v167
	v_mov_b32_e32 v32, v168
	v_mov_b32_e32 v64, v169
	v_mov_b32_e32 v38, v170
	v_mov_b32_e32 v66, v171
	v_mov_b32_e32 v10, v172
	v_pk_add_f32 v[68:69], v[14:15], v[42:43]
	v_pk_add_f32 v[14:15], v[14:15], v[42:43] neg_lo:[0,1] neg_hi:[0,1]
	s_nop 0
	v_mov_b32_e32 v13, v15
	v_mov_b32_e32 v10, v14
	v_mov_b32_e32 v42, v15
	v_mov_b32_e32 v43, v11
	v_pk_mul_f32 v[14:15], v[12:13], v[66:67] op_sel_hi:[1,0] neg_lo:[0,1] neg_hi:[0,1]
	v_pk_add_f32 v[70:71], v[18:19], v[52:53]
	v_pk_fma_f32 v[42:43], v[42:43], v[60:61], v[14:15] op_sel_hi:[1,0,1]
	v_pk_add_f32 v[14:15], v[16:17], v[48:49]
	v_pk_add_f32 v[48:49], v[16:17], v[48:49] neg_lo:[0,1] neg_hi:[0,1]
	v_mov_b32_e32 v17, v11
	v_mov_b32_e32 v13, v48
	v_mov_b32_e32 v16, v48
	v_pk_mul_f32 v[54:55], v[12:13], v[38:39] op_sel_hi:[1,0] neg_lo:[0,1] neg_hi:[0,1]
	v_mov_b32_e32 v13, v49
	v_pk_add_f32 v[18:19], v[18:19], v[52:53] neg_lo:[0,1] neg_hi:[0,1]
	v_pk_fma_f32 v[16:17], v[16:17], v[34:35], v[54:55] op_sel_hi:[1,0,1]
	v_mov_b32_e32 v54, v49
	v_mov_b32_e32 v55, v11
	v_pk_mul_f32 v[48:49], v[12:13], v[64:65] op_sel_hi:[1,0] neg_lo:[0,1] neg_hi:[0,1]
	v_mov_b32_e32 v13, v18
	v_pk_fma_f32 v[48:49], v[54:55], v[62:63], v[48:49] op_sel_hi:[1,0,1]
	v_mov_b32_e32 v52, v18
	v_mov_b32_e32 v53, v11
	v_pk_mul_f32 v[54:55], v[12:13], v[32:33] op_sel_hi:[1,0] neg_lo:[0,1] neg_hi:[0,1]
	v_mov_b32_e32 v13, v19
	v_pk_fma_f32 v[52:53], v[52:53], v[32:33], v[54:55] op_sel_hi:[1,0,1]
	v_mov_b32_e32 v54, v19
	v_mov_b32_e32 v55, v11
	v_pk_add_f32 v[18:19], v[20:21], v[50:51]
	v_pk_add_f32 v[20:21], v[20:21], v[50:51] neg_lo:[0,1] neg_hi:[0,1]
	v_pk_mul_f32 v[54:55], v[54:55], v[64:65] op_sel_hi:[1,0]
	v_mov_b32_e32 v50, v20
	v_mov_b32_e32 v51, v11
	v_pk_fma_f32 v[54:55], v[12:13], v[62:63], v[54:55] op_sel_hi:[1,0,1] neg_lo:[0,1,0] neg_hi:[0,1,0]
	v_pk_mul_f32 v[50:51], v[50:51], v[38:39] op_sel_hi:[1,0]
	v_mov_b32_e32 v13, v20
	v_pk_fma_f32 v[58:59], v[12:13], v[34:35], v[50:51] op_sel_hi:[1,0,1] neg_lo:[0,1,0] neg_hi:[0,1,0]
	v_mov_b32_e32 v50, v21
	v_mov_b32_e32 v51, v11
	v_pk_mul_f32 v[50:51], v[50:51], v[66:67] op_sel_hi:[1,0]
	v_mov_b32_e32 v13, v21
	v_pk_add_f32 v[20:21], v[24:25], v[46:47]
	v_pk_add_f32 v[24:25], v[24:25], v[46:47] neg_lo:[0,1] neg_hi:[0,1]
	v_pk_fma_f32 v[56:57], v[12:13], v[60:61], v[50:51] op_sel_hi:[1,0,1] neg_lo:[0,1,0] neg_hi:[0,1,0]
	v_xor_b32_e32 v73, 0x80000000, v24
	v_mov_b32_e32 v46, v25
	v_mov_b32_e32 v47, v11
	v_mov_b32_e32 v13, v25
	v_pk_add_f32 v[24:25], v[28:29], v[44:45]
	v_pk_add_f32 v[28:29], v[28:29], v[44:45] neg_lo:[0,1] neg_hi:[0,1]
	v_pk_mul_f32 v[46:47], v[46:47], v[66:67] op_sel_hi:[1,0] neg_lo:[0,1] neg_hi:[0,1]
	v_mov_b32_e32 v44, v28
	v_mov_b32_e32 v45, v11
	v_pk_fma_f32 v[74:75], v[12:13], v[60:61], v[46:47] op_sel_hi:[1,0,1] neg_lo:[0,1,0] neg_hi:[0,1,0]
	v_pk_mul_f32 v[44:45], v[44:45], v[38:39] op_sel_hi:[1,0] neg_lo:[0,1] neg_hi:[0,1]
	v_mov_b32_e32 v13, v28
	v_pk_fma_f32 v[76:77], v[12:13], v[34:35], v[44:45] op_sel_hi:[1,0,1] neg_lo:[0,1,0] neg_hi:[0,1,0]
	v_mov_b32_e32 v44, v29
	v_mov_b32_e32 v45, v11
	v_pk_mul_f32 v[44:45], v[44:45], v[64:65] op_sel_hi:[1,0] neg_lo:[0,1] neg_hi:[0,1]
	v_mov_b32_e32 v13, v29
	v_pk_add_f32 v[28:29], v[30:31], v[40:41]
	v_pk_add_f32 v[30:31], v[30:31], v[40:41] neg_lo:[0,1] neg_hi:[0,1]
	v_pk_fma_f32 v[78:79], v[12:13], v[62:63], v[44:45] op_sel_hi:[1,0,1] neg_lo:[0,1,0] neg_hi:[0,1,0]
	v_mov_b32_e32 v13, v30
	v_mov_b32_e32 v40, v30
	v_mov_b32_e32 v41, v11
	v_pk_mul_f32 v[44:45], v[12:13], v[32:33] op_sel_hi:[1,0] neg_lo:[0,1] neg_hi:[0,1]
	v_mov_b32_e32 v13, v31
	v_pk_fma_f32 v[80:81], v[40:41], v[32:33], v[44:45] op_sel_hi:[1,0,1] neg_lo:[0,1,0] neg_hi:[0,1,0]
	v_mov_b32_e32 v40, v31
	v_pk_mul_f32 v[30:31], v[12:13], v[64:65] op_sel_hi:[1,0] neg_lo:[0,1] neg_hi:[0,1]
	v_mov_b32_e32 v84, v11
	v_pk_fma_f32 v[62:63], v[40:41], v[62:63], v[30:31] op_sel_hi:[1,0,1] neg_lo:[0,1,0] neg_hi:[0,1,0]
	v_pk_add_f32 v[30:31], v[26:27], v[36:37]
	v_pk_add_f32 v[26:27], v[26:27], v[36:37] neg_lo:[0,1] neg_hi:[0,1]
	v_mov_b32_e32 v37, v11
	v_mov_b32_e32 v13, v26
	v_mov_b32_e32 v36, v26
	v_pk_mul_f32 v[40:41], v[12:13], v[38:39] op_sel_hi:[1,0] neg_lo:[0,1] neg_hi:[0,1]
	v_mov_b32_e32 v13, v27
	v_pk_fma_f32 v[64:65], v[36:37], v[34:35], v[40:41] op_sel_hi:[1,0,1] neg_lo:[0,1,0] neg_hi:[0,1,0]
	v_mov_b32_e32 v36, v27
	v_pk_mul_f32 v[26:27], v[12:13], v[66:67] op_sel_hi:[1,0] neg_lo:[0,1] neg_hi:[0,1]
	v_mov_b32_e32 v41, v11
	v_pk_fma_f32 v[66:67], v[36:37], v[60:61], v[26:27] op_sel_hi:[1,0,1] neg_lo:[0,1,0] neg_hi:[0,1,0]
	v_pk_add_f32 v[26:27], v[68:69], v[20:21] neg_lo:[0,1] neg_hi:[0,1]
	v_pk_add_f32 v[20:21], v[68:69], v[20:21]
	v_mov_b32_e32 v13, v27
	v_mov_b32_e32 v36, v26
	v_mov_b32_e32 v40, v27
	v_pk_mul_f32 v[26:27], v[12:13], v[38:39] op_sel_hi:[1,0] neg_lo:[0,1] neg_hi:[0,1]
	v_mov_b32_e32 v61, v11
	v_pk_fma_f32 v[44:45], v[40:41], v[34:35], v[26:27] op_sel_hi:[1,0,1]
	v_pk_add_f32 v[26:27], v[14:15], v[24:25] neg_lo:[0,1] neg_hi:[0,1]
	v_pk_add_f32 v[14:15], v[14:15], v[24:25]
	v_mov_b32_e32 v13, v26
	v_mov_b32_e32 v40, v26
	v_pk_mul_f32 v[46:47], v[12:13], v[32:33] op_sel_hi:[1,0] neg_lo:[0,1] neg_hi:[0,1]
	v_mov_b32_e32 v13, v27
	v_pk_fma_f32 v[50:51], v[40:41], v[32:33], v[46:47] op_sel_hi:[1,0,1]
	v_mov_b32_e32 v40, v27
	v_pk_mul_f32 v[40:41], v[40:41], v[38:39] op_sel_hi:[1,0]
	v_pk_add_f32 v[26:27], v[70:71], v[28:29] neg_lo:[0,1] neg_hi:[0,1]
	v_pk_fma_f32 v[82:83], v[12:13], v[34:35], v[40:41] op_sel_hi:[1,0,1] neg_lo:[0,1,0] neg_hi:[0,1,0]
	v_mov_b32_e32 v40, v27
	v_mov_b32_e32 v41, v11
	v_xor_b32_e32 v85, 0x80000000, v26
	v_pk_mul_f32 v[40:41], v[40:41], v[38:39] op_sel_hi:[1,0] neg_lo:[0,1] neg_hi:[0,1]
	v_mov_b32_e32 v13, v27
	v_pk_add_f32 v[26:27], v[18:19], v[30:31] neg_lo:[0,1] neg_hi:[0,1]
	v_pk_fma_f32 v[86:87], v[12:13], v[34:35], v[40:41] op_sel_hi:[1,0,1] neg_lo:[0,1,0] neg_hi:[0,1,0]
	v_mov_b32_e32 v13, v26
	v_mov_b32_e32 v40, v26
	v_mov_b32_e32 v41, v11
	v_pk_mul_f32 v[46:47], v[12:13], v[32:33] op_sel_hi:[1,0] neg_lo:[0,1] neg_hi:[0,1]
	v_mov_b32_e32 v13, v27
	v_pk_fma_f32 v[88:89], v[40:41], v[32:33], v[46:47] op_sel_hi:[1,0,1] neg_lo:[0,1,0] neg_hi:[0,1,0]
	v_mov_b32_e32 v40, v27
	v_pk_mul_f32 v[26:27], v[12:13], v[38:39] op_sel_hi:[1,0] neg_lo:[0,1] neg_hi:[0,1]
	v_pk_add_f32 v[24:25], v[70:71], v[28:29]
	v_pk_fma_f32 v[90:91], v[40:41], v[34:35], v[26:27] op_sel_hi:[1,0,1] neg_lo:[0,1,0] neg_hi:[0,1,0]
	v_pk_add_f32 v[26:27], v[20:21], v[24:25] neg_lo:[0,1] neg_hi:[0,1]
	v_pk_add_f32 v[18:19], v[18:19], v[30:31]
	v_mov_b32_e32 v13, v27
	v_mov_b32_e32 v28, v26
	v_pk_add_f32 v[20:21], v[20:21], v[24:25]
	v_mov_b32_e32 v24, v27
	v_mov_b32_e32 v25, v11
	v_pk_mul_f32 v[26:27], v[12:13], v[32:33] op_sel_hi:[1,0] neg_lo:[0,1] neg_hi:[0,1]
	v_mov_b32_e32 v29, v11
	v_pk_fma_f32 v[24:25], v[24:25], v[32:33], v[26:27] op_sel_hi:[1,0,1]
	v_pk_add_f32 v[26:27], v[14:15], v[18:19] neg_lo:[0,1] neg_hi:[0,1]
	v_pk_add_f32 v[14:15], v[14:15], v[18:19]
	v_mov_b32_e32 v13, v27
	v_xor_b32_e32 v41, 0x80000000, v26
	v_mov_b32_e32 v18, v27
	v_mov_b32_e32 v19, v11
	v_pk_mul_f32 v[26:27], v[12:13], v[32:33] op_sel_hi:[1,0] neg_lo:[0,1] neg_hi:[0,1]
	v_pk_add_f32 v[30:31], v[20:21], v[14:15]
	v_pk_fma_f32 v[18:19], v[18:19], v[32:33], v[26:27] op_sel_hi:[1,0,1] neg_lo:[0,1,0] neg_hi:[0,1,0]
	v_pk_add_f32 v[26:27], v[20:21], v[14:15] neg_lo:[0,1] neg_hi:[0,1]
	v_mov_b32_e32 v40, v11
	v_pk_add_f32 v[14:15], v[26:27], 0 neg_lo:[1,1] neg_hi:[1,1]
	v_mov_b32_e32 v60, v26
	v_mov_b32_e32 v14, v11
	v_pk_add_f32 v[26:27], v[24:25], v[18:19]
	v_pk_add_f32 v[18:19], v[24:25], v[18:19] neg_lo:[0,1] neg_hi:[0,1]
	v_pk_add_f32 v[46:47], v[60:61], v[14:15]
	v_pk_add_f32 v[20:21], v[60:61], v[14:15] neg_lo:[0,1] neg_hi:[0,1]
	v_pk_add_f32 v[14:15], v[28:29], v[40:41]
	v_pk_add_f32 v[28:29], v[28:29], v[40:41] neg_lo:[0,1] neg_hi:[0,1]
	v_xor_b32_e32 v25, 0x80000000, v18
	v_mov_b32_e32 v24, v19
	v_pk_add_f32 v[60:61], v[14:15], v[26:27]
	v_pk_add_f32 v[26:27], v[14:15], v[26:27] neg_lo:[0,1] neg_hi:[0,1]
	v_pk_add_f32 v[40:41], v[28:29], v[24:25]
	v_pk_add_f32 v[14:15], v[28:29], v[24:25] neg_lo:[0,1] neg_hi:[0,1]
	v_pk_add_f32 v[18:19], v[36:37], v[84:85]
	v_pk_add_f32 v[28:29], v[36:37], v[84:85] neg_lo:[0,1] neg_hi:[0,1]
	v_pk_add_f32 v[36:37], v[44:45], v[86:87] neg_lo:[0,1] neg_hi:[0,1]
	v_pk_add_f32 v[24:25], v[44:45], v[86:87]
	v_xor_b32_e32 v44, 0x80000000, v37
	v_mov_b32_e32 v45, v36
	v_pk_mul_f32 v[44:45], v[32:33], v[44:45] op_sel_hi:[0,1] neg_lo:[1,0] neg_hi:[1,0]
	v_pk_fma_f32 v[44:45], v[32:33], v[36:37], v[44:45] op_sel_hi:[0,1,1]
	v_pk_add_f32 v[36:37], v[50:51], v[88:89]
	v_pk_add_f32 v[50:51], v[50:51], v[88:89] neg_lo:[0,1] neg_hi:[0,1]
	v_pk_add_f32 v[70:71], v[82:83], v[90:91] neg_lo:[0,1] neg_hi:[0,1]
	v_xor_b32_e32 v69, 0x80000000, v50
	v_mov_b32_e32 v68, v51
	v_pk_add_f32 v[50:51], v[82:83], v[90:91]
	v_xor_b32_e32 v82, 0x80000000, v71
	v_mov_b32_e32 v83, v70
	v_pk_mul_f32 v[82:83], v[32:33], v[82:83] op_sel_hi:[0,1] neg_lo:[1,0] neg_hi:[1,0]
	v_pk_fma_f32 v[70:71], v[32:33], v[70:71], v[82:83] op_sel_hi:[0,1,1] neg_lo:[1,0,0] neg_hi:[1,0,0]
	v_pk_add_f32 v[82:83], v[18:19], v[36:37]
	v_pk_add_f32 v[18:19], v[18:19], v[36:37] neg_lo:[0,1] neg_hi:[0,1]
	v_pk_add_f32 v[36:37], v[24:25], v[50:51]
	v_pk_add_f32 v[24:25], v[24:25], v[50:51] neg_lo:[0,1] neg_hi:[0,1]
	v_mov_b32_e32 v72, v11
	v_xor_b32_e32 v85, 0x80000000, v24
	v_mov_b32_e32 v84, v25
	v_pk_add_f32 v[50:51], v[18:19], v[84:85]
	v_pk_add_f32 v[24:25], v[18:19], v[84:85] neg_lo:[0,1] neg_hi:[0,1]
	v_pk_add_f32 v[18:19], v[28:29], v[68:69]
	v_pk_add_f32 v[68:69], v[28:29], v[68:69] neg_lo:[0,1] neg_hi:[0,1]
	v_pk_add_f32 v[28:29], v[44:45], v[70:71]
	v_pk_add_f32 v[44:45], v[44:45], v[70:71] neg_lo:[0,1] neg_hi:[0,1]
	v_pk_add_f32 v[86:87], v[82:83], v[36:37]
	v_xor_b32_e32 v71, 0x80000000, v44
	v_mov_b32_e32 v70, v45
	v_pk_add_f32 v[36:37], v[82:83], v[36:37] neg_lo:[0,1] neg_hi:[0,1]
	v_pk_add_f32 v[82:83], v[18:19], v[28:29]
	v_pk_add_f32 v[28:29], v[18:19], v[28:29] neg_lo:[0,1] neg_hi:[0,1]
	v_pk_add_f32 v[44:45], v[68:69], v[70:71]
	v_pk_add_f32 v[18:19], v[68:69], v[70:71] neg_lo:[0,1] neg_hi:[0,1]
	v_pk_add_f32 v[68:69], v[10:11], v[72:73]
	v_pk_add_f32 v[70:71], v[10:11], v[72:73] neg_lo:[0,1] neg_hi:[0,1]
	v_pk_add_f32 v[72:73], v[42:43], v[74:75]
	v_pk_add_f32 v[42:43], v[42:43], v[74:75] neg_lo:[0,1] neg_hi:[0,1]
	v_add_f32_e32 v10, v30, v31
	v_xor_b32_e32 v74, 0x80000000, v43
	v_mov_b32_e32 v75, v42
	v_pk_mul_f32 v[74:75], v[38:39], v[74:75] op_sel_hi:[0,1] neg_lo:[1,0] neg_hi:[1,0]
	v_pk_fma_f32 v[42:43], v[34:35], v[42:43], v[74:75] op_sel_hi:[0,1,1]
	v_pk_add_f32 v[74:75], v[16:17], v[76:77]
	v_pk_add_f32 v[16:17], v[16:17], v[76:77] neg_lo:[0,1] neg_hi:[0,1]
	v_lshl_add_u32 v13, v92, 3, 0
	v_xor_b32_e32 v76, 0x80000000, v17
	v_mov_b32_e32 v77, v16
	v_pk_mul_f32 v[76:77], v[32:33], v[76:77] op_sel_hi:[0,1] neg_lo:[1,0] neg_hi:[1,0]
	v_pk_fma_f32 v[16:17], v[32:33], v[16:17], v[76:77] op_sel_hi:[0,1,1]
	v_pk_add_f32 v[76:77], v[48:49], v[78:79]
	v_pk_add_f32 v[48:49], v[48:49], v[78:79] neg_lo:[0,1] neg_hi:[0,1]
	s_nop 0
	v_xor_b32_e32 v78, 0x80000000, v49
	v_mov_b32_e32 v79, v48
	v_pk_mul_f32 v[78:79], v[34:35], v[78:79] op_sel_hi:[0,1] neg_lo:[1,0] neg_hi:[1,0]
	v_pk_fma_f32 v[78:79], v[38:39], v[48:49], v[78:79] op_sel_hi:[0,1,1]
	v_pk_add_f32 v[48:49], v[52:53], v[80:81]
	v_pk_add_f32 v[52:53], v[52:53], v[80:81] neg_lo:[0,1] neg_hi:[0,1]
	s_nop 0
	v_xor_b32_e32 v81, 0x80000000, v52
	v_mov_b32_e32 v80, v53
	v_pk_add_f32 v[52:53], v[54:55], v[62:63]
	v_pk_add_f32 v[54:55], v[54:55], v[62:63] neg_lo:[0,1] neg_hi:[0,1]
	s_nop 0
	v_xor_b32_e32 v62, 0x80000000, v55
	v_mov_b32_e32 v63, v54
	v_pk_mul_f32 v[62:63], v[34:35], v[62:63] op_sel_hi:[0,1] neg_lo:[1,0] neg_hi:[1,0]
	v_pk_fma_f32 v[62:63], v[38:39], v[54:55], v[62:63] op_sel_hi:[0,1,1] neg_lo:[1,0,0] neg_hi:[1,0,0]
	v_pk_add_f32 v[54:55], v[58:59], v[64:65]
	v_pk_add_f32 v[58:59], v[58:59], v[64:65] neg_lo:[0,1] neg_hi:[0,1]
	s_nop 0
	v_xor_b32_e32 v64, 0x80000000, v59
	v_mov_b32_e32 v65, v58
	v_pk_mul_f32 v[64:65], v[32:33], v[64:65] op_sel_hi:[0,1] neg_lo:[1,0] neg_hi:[1,0]
	v_pk_fma_f32 v[58:59], v[32:33], v[58:59], v[64:65] op_sel_hi:[0,1,1] neg_lo:[1,0,0] neg_hi:[1,0,0]
	v_pk_add_f32 v[64:65], v[56:57], v[66:67]
	v_pk_add_f32 v[56:57], v[56:57], v[66:67] neg_lo:[0,1] neg_hi:[0,1]
	s_nop 0
	v_xor_b32_e32 v66, 0x80000000, v57
	v_mov_b32_e32 v67, v56
	v_pk_mul_f32 v[38:39], v[38:39], v[66:67] op_sel_hi:[0,1] neg_lo:[1,0] neg_hi:[1,0]
	v_pk_fma_f32 v[56:57], v[34:35], v[56:57], v[38:39] op_sel_hi:[0,1,1] neg_lo:[1,0,0] neg_hi:[1,0,0]
	v_pk_add_f32 v[38:39], v[52:53], v[72:73]
	v_pk_add_f32 v[52:53], v[72:73], v[52:53] neg_lo:[0,1] neg_hi:[0,1]
	v_pk_add_f32 v[34:35], v[68:69], v[48:49]
	v_xor_b32_e32 v66, 0x80000000, v53
	v_mov_b32_e32 v67, v52
	v_pk_mul_f32 v[66:67], v[32:33], v[66:67] op_sel_hi:[0,1] neg_lo:[1,0] neg_hi:[1,0]
	v_pk_fma_f32 v[52:53], v[32:33], v[52:53], v[66:67] op_sel_hi:[0,1,1]
	v_pk_add_f32 v[66:67], v[74:75], v[54:55]
	v_pk_add_f32 v[54:55], v[74:75], v[54:55] neg_lo:[0,1] neg_hi:[0,1]
	v_pk_add_f32 v[48:49], v[68:69], v[48:49] neg_lo:[0,1] neg_hi:[0,1]
	v_xor_b32_e32 v69, 0x80000000, v54
	v_mov_b32_e32 v68, v55
	v_pk_add_f32 v[54:55], v[76:77], v[64:65]
	v_pk_add_f32 v[64:65], v[76:77], v[64:65] neg_lo:[0,1] neg_hi:[0,1]
	s_nop 0
	v_xor_b32_e32 v72, 0x80000000, v65
	v_mov_b32_e32 v73, v64
	v_pk_mul_f32 v[72:73], v[32:33], v[72:73] op_sel_hi:[0,1] neg_lo:[1,0] neg_hi:[1,0]
	v_pk_fma_f32 v[64:65], v[32:33], v[64:65], v[72:73] op_sel_hi:[0,1,1] neg_lo:[1,0,0] neg_hi:[1,0,0]
	v_pk_add_f32 v[72:73], v[34:35], v[66:67]
	v_pk_add_f32 v[34:35], v[34:35], v[66:67] neg_lo:[0,1] neg_hi:[0,1]
	v_pk_add_f32 v[66:67], v[38:39], v[54:55]
	v_pk_add_f32 v[38:39], v[38:39], v[54:55] neg_lo:[0,1] neg_hi:[0,1]
	v_pk_add_f32 v[76:77], v[72:73], v[66:67]
	v_xor_b32_e32 v75, 0x80000000, v38
	v_mov_b32_e32 v74, v39
	v_pk_add_f32 v[54:55], v[72:73], v[66:67] neg_lo:[0,1] neg_hi:[0,1]
	v_pk_add_f32 v[66:67], v[34:35], v[74:75]
	v_pk_add_f32 v[38:39], v[34:35], v[74:75] neg_lo:[0,1] neg_hi:[0,1]
	v_pk_add_f32 v[34:35], v[48:49], v[68:69]
	v_pk_add_f32 v[68:69], v[48:49], v[68:69] neg_lo:[0,1] neg_hi:[0,1]
	v_pk_add_f32 v[48:49], v[52:53], v[64:65]
	v_pk_add_f32 v[52:53], v[52:53], v[64:65] neg_lo:[0,1] neg_hi:[0,1]
	v_pk_add_f32 v[72:73], v[34:35], v[48:49]
	v_xor_b32_e32 v65, 0x80000000, v52
	v_mov_b32_e32 v64, v53
	v_pk_add_f32 v[48:49], v[34:35], v[48:49] neg_lo:[0,1] neg_hi:[0,1]
	v_pk_add_f32 v[74:75], v[68:69], v[64:65]
	v_pk_add_f32 v[34:35], v[68:69], v[64:65] neg_lo:[0,1] neg_hi:[0,1]
	v_pk_add_f32 v[68:69], v[62:63], v[42:43]
	v_pk_add_f32 v[42:43], v[42:43], v[62:63] neg_lo:[0,1] neg_hi:[0,1]
	v_pk_add_f32 v[52:53], v[70:71], v[80:81]
	v_xor_b32_e32 v62, 0x80000000, v43
	v_mov_b32_e32 v63, v42
	v_pk_mul_f32 v[62:63], v[32:33], v[62:63] op_sel_hi:[0,1] neg_lo:[1,0] neg_hi:[1,0]
	v_pk_fma_f32 v[62:63], v[32:33], v[42:43], v[62:63] op_sel_hi:[0,1,1]
	v_pk_add_f32 v[42:43], v[16:17], v[58:59]
	v_pk_add_f32 v[16:17], v[16:17], v[58:59] neg_lo:[0,1] neg_hi:[0,1]
	v_pk_add_f32 v[64:65], v[70:71], v[80:81] neg_lo:[0,1] neg_hi:[0,1]
	v_xor_b32_e32 v59, 0x80000000, v16
	v_mov_b32_e32 v58, v17
	v_pk_add_f32 v[16:17], v[78:79], v[56:57]
	v_pk_add_f32 v[56:57], v[78:79], v[56:57] neg_lo:[0,1] neg_hi:[0,1]
	s_nop 0
	v_xor_b32_e32 v70, 0x80000000, v57
	v_mov_b32_e32 v71, v56
	v_pk_mul_f32 v[70:71], v[32:33], v[70:71] op_sel_hi:[0,1] neg_lo:[1,0] neg_hi:[1,0]
	v_pk_fma_f32 v[32:33], v[32:33], v[56:57], v[70:71] op_sel_hi:[0,1,1] neg_lo:[1,0,0] neg_hi:[1,0,0]
	v_pk_add_f32 v[56:57], v[52:53], v[42:43]
	v_pk_add_f32 v[42:43], v[52:53], v[42:43] neg_lo:[0,1] neg_hi:[0,1]
	v_pk_add_f32 v[52:53], v[68:69], v[16:17]
	v_pk_add_f32 v[16:17], v[68:69], v[16:17] neg_lo:[0,1] neg_hi:[0,1]
	v_pk_add_f32 v[70:71], v[56:57], v[52:53]
	v_xor_b32_e32 v69, 0x80000000, v16
	v_mov_b32_e32 v68, v17
	v_pk_add_f32 v[56:57], v[56:57], v[52:53] neg_lo:[0,1] neg_hi:[0,1]
	v_pk_add_f32 v[16:17], v[64:65], v[58:59]
	v_pk_add_f32 v[52:53], v[62:63], v[32:33]
	v_pk_add_f32 v[32:33], v[62:63], v[32:33] neg_lo:[0,1] neg_hi:[0,1]
	v_pk_add_f32 v[58:59], v[64:65], v[58:59] neg_lo:[0,1] neg_hi:[0,1]
	v_xor_b32_e32 v63, 0x80000000, v32
	v_mov_b32_e32 v62, v33
	v_pk_add_f32 v[64:65], v[16:17], v[52:53]
	v_pk_add_f32 v[52:53], v[16:17], v[52:53] neg_lo:[0,1] neg_hi:[0,1]
	v_mov_b64_e32 v[16:17], s[92:93]
	v_pk_add_f32 v[78:79], v[42:43], v[68:69]
	v_pk_add_f32 v[42:43], v[42:43], v[68:69] neg_lo:[0,1] neg_hi:[0,1]
	v_pk_add_f32 v[68:69], v[58:59], v[62:63]
	v_pk_add_f32 v[32:33], v[58:59], v[62:63] neg_lo:[0,1] neg_hi:[0,1]
	v_pk_fma_f32 v[58:59], v[10:11], s[42:43], v[16:17] op_sel_hi:[0,1,1]
	ds_write_b64 v13, v[58:59]
	v_pk_fma_f32 v[58:59], v[22:23], s[92:93], v[22:23] op_sel:[1,0,0] op_sel_hi:[0,1,1]
	v_xor_b32_e32 v62, 0x80000000, v77
	v_mov_b32_e32 v63, v77
	v_pk_mul_f32 v[62:63], v[58:59], v[62:63] op_sel:[1,0] op_sel_hi:[0,1]
	v_pk_fma_f32 v[62:63], v[58:59], v[76:77], v[62:63] op_sel_hi:[1,0,1]
	ds_write_b64 v13, v[62:63] offset:4224
	v_xor_b32_e32 v62, 0x80000000, v59
	v_mov_b32_e32 v63, v59
	v_pk_mul_f32 v[62:63], v[22:23], v[62:63] op_sel:[1,0] op_sel_hi:[0,1]
	v_pk_fma_f32 v[58:59], v[22:23], v[58:59], v[62:63] op_sel_hi:[1,0,1]
	v_xor_b32_e32 v62, 0x80000000, v87
	v_mov_b32_e32 v63, v87
	v_pk_mul_f32 v[62:63], v[58:59], v[62:63] op_sel:[1,0] op_sel_hi:[0,1]
	v_pk_fma_f32 v[62:63], v[58:59], v[86:87], v[62:63] op_sel_hi:[1,0,1]
	ds_write_b64 v13, v[62:63] offset:8448
	v_xor_b32_e32 v62, 0x80000000, v59
	v_mov_b32_e32 v63, v59
	v_pk_mul_f32 v[62:63], v[22:23], v[62:63] op_sel:[1,0] op_sel_hi:[0,1]
	v_pk_fma_f32 v[58:59], v[22:23], v[58:59], v[62:63] op_sel_hi:[1,0,1]
	v_xor_b32_e32 v62, 0x80000000, v71
	v_mov_b32_e32 v63, v71
	v_pk_mul_f32 v[62:63], v[58:59], v[62:63] op_sel:[1,0] op_sel_hi:[0,1]
	v_pk_fma_f32 v[62:63], v[58:59], v[70:71], v[62:63] op_sel_hi:[1,0,1]
	ds_write_b64 v13, v[62:63] offset:12672
	v_xor_b32_e32 v62, 0x80000000, v59
	v_mov_b32_e32 v63, v59
	v_pk_mul_f32 v[62:63], v[22:23], v[62:63] op_sel:[1,0] op_sel_hi:[0,1]
	v_pk_fma_f32 v[58:59], v[22:23], v[58:59], v[62:63] op_sel_hi:[1,0,1]
	v_xor_b32_e32 v62, 0x80000000, v61
	v_mov_b32_e32 v63, v61
	v_pk_mul_f32 v[62:63], v[62:63], v[58:59] op_sel:[0,1] op_sel_hi:[1,0]
	s_nop 0
	v_pk_fma_f32 v[60:61], v[60:61], v[58:59], v[62:63] op_sel_hi:[0,1,1]
	ds_write_b64 v13, v[60:61] offset:16896
	v_xor_b32_e32 v60, 0x80000000, v59
	v_mov_b32_e32 v61, v59
	v_pk_mul_f32 v[60:61], v[22:23], v[60:61] op_sel:[1,0] op_sel_hi:[0,1]
	v_pk_fma_f32 v[58:59], v[22:23], v[58:59], v[60:61] op_sel_hi:[1,0,1]
	v_xor_b32_e32 v60, 0x80000000, v73
	v_mov_b32_e32 v61, v73
	v_pk_mul_f32 v[60:61], v[58:59], v[60:61] op_sel:[1,0] op_sel_hi:[0,1]
	v_pk_fma_f32 v[60:61], v[58:59], v[72:73], v[60:61] op_sel_hi:[1,0,1]
	ds_write_b64 v13, v[60:61] offset:21120
	v_xor_b32_e32 v60, 0x80000000, v59
	v_mov_b32_e32 v61, v59
	v_pk_mul_f32 v[60:61], v[22:23], v[60:61] op_sel:[1,0] op_sel_hi:[0,1]
	v_pk_fma_f32 v[58:59], v[22:23], v[58:59], v[60:61] op_sel_hi:[1,0,1]
	v_xor_b32_e32 v60, 0x80000000, v83
	v_mov_b32_e32 v61, v83
	v_pk_mul_f32 v[60:61], v[60:61], v[58:59] op_sel:[0,1] op_sel_hi:[1,0]
	s_nop 0
	v_pk_fma_f32 v[60:61], v[82:83], v[58:59], v[60:61] op_sel_hi:[0,1,1]
	ds_write_b64 v13, v[60:61] offset:25344
	v_xor_b32_e32 v60, 0x80000000, v59
	v_mov_b32_e32 v61, v59
	v_pk_mul_f32 v[60:61], v[22:23], v[60:61] op_sel:[1,0] op_sel_hi:[0,1]
	v_pk_fma_f32 v[58:59], v[22:23], v[58:59], v[60:61] op_sel_hi:[1,0,1]
	v_xor_b32_e32 v60, 0x80000000, v65
	v_mov_b32_e32 v61, v65
	v_pk_mul_f32 v[60:61], v[60:61], v[58:59] op_sel:[0,1] op_sel_hi:[1,0]
	s_nop 0
	v_pk_fma_f32 v[60:61], v[64:65], v[58:59], v[60:61] op_sel_hi:[0,1,1]
	ds_write_b64 v13, v[60:61] offset:29568
	v_xor_b32_e32 v60, 0x80000000, v59
	v_mov_b32_e32 v61, v59
	v_pk_mul_f32 v[60:61], v[22:23], v[60:61] op_sel:[1,0] op_sel_hi:[0,1]
	v_pk_fma_f32 v[58:59], v[22:23], v[58:59], v[60:61] op_sel_hi:[1,0,1]
	v_xor_b32_e32 v60, 0x80000000, v47
	v_mov_b32_e32 v61, v47
	v_pk_mul_f32 v[60:61], v[60:61], v[58:59] op_sel:[0,1] op_sel_hi:[1,0]
	s_nop 0
	v_pk_fma_f32 v[46:47], v[46:47], v[58:59], v[60:61] op_sel_hi:[0,1,1]
	ds_write_b64 v13, v[46:47] offset:33792
	v_xor_b32_e32 v46, 0x80000000, v59
	v_mov_b32_e32 v47, v59
	v_pk_mul_f32 v[46:47], v[22:23], v[46:47] op_sel:[1,0] op_sel_hi:[0,1]
	v_pk_fma_f32 v[46:47], v[22:23], v[58:59], v[46:47] op_sel_hi:[1,0,1]
	v_xor_b32_e32 v58, 0x80000000, v67
	v_mov_b32_e32 v59, v67
	v_pk_mul_f32 v[58:59], v[58:59], v[46:47] op_sel:[0,1] op_sel_hi:[1,0]
	s_nop 0
	v_pk_fma_f32 v[58:59], v[66:67], v[46:47], v[58:59] op_sel_hi:[0,1,1]
	ds_write_b64 v13, v[58:59] offset:38016
	v_xor_b32_e32 v58, 0x80000000, v47
	v_mov_b32_e32 v59, v47
	v_pk_mul_f32 v[58:59], v[22:23], v[58:59] op_sel:[1,0] op_sel_hi:[0,1]
	v_pk_fma_f32 v[46:47], v[22:23], v[46:47], v[58:59] op_sel_hi:[1,0,1]
	v_xor_b32_e32 v58, 0x80000000, v51
	v_mov_b32_e32 v59, v51
	v_pk_mul_f32 v[58:59], v[58:59], v[46:47] op_sel:[0,1] op_sel_hi:[1,0]
	s_nop 0
	v_pk_fma_f32 v[50:51], v[50:51], v[46:47], v[58:59] op_sel_hi:[0,1,1]
	ds_write_b64 v13, v[50:51] offset:42240
	v_xor_b32_e32 v50, 0x80000000, v47
	v_mov_b32_e32 v51, v47
	v_pk_mul_f32 v[50:51], v[22:23], v[50:51] op_sel:[1,0] op_sel_hi:[0,1]
	v_pk_fma_f32 v[46:47], v[22:23], v[46:47], v[50:51] op_sel_hi:[1,0,1]
	v_xor_b32_e32 v50, 0x80000000, v79
	v_mov_b32_e32 v51, v79
	v_pk_mul_f32 v[50:51], v[50:51], v[46:47] op_sel:[0,1] op_sel_hi:[1,0]
	s_nop 0
	v_pk_fma_f32 v[50:51], v[78:79], v[46:47], v[50:51] op_sel_hi:[0,1,1]
	ds_write_b64 v13, v[50:51] offset:46464
	v_xor_b32_e32 v50, 0x80000000, v47
	v_mov_b32_e32 v51, v47
	v_pk_mul_f32 v[50:51], v[22:23], v[50:51] op_sel:[1,0] op_sel_hi:[0,1]
	v_pk_fma_f32 v[46:47], v[22:23], v[46:47], v[50:51] op_sel_hi:[1,0,1]
	v_xor_b32_e32 v50, 0x80000000, v41
	v_mov_b32_e32 v51, v41
	v_pk_mul_f32 v[50:51], v[50:51], v[46:47] op_sel:[0,1] op_sel_hi:[1,0]
	s_nop 0
	v_pk_fma_f32 v[40:41], v[40:41], v[46:47], v[50:51] op_sel_hi:[0,1,1]
	ds_write_b64 v13, v[40:41] offset:50688
	v_xor_b32_e32 v40, 0x80000000, v47
	v_mov_b32_e32 v41, v47
	v_pk_mul_f32 v[40:41], v[22:23], v[40:41] op_sel:[1,0] op_sel_hi:[0,1]
	v_pk_fma_f32 v[40:41], v[22:23], v[46:47], v[40:41] op_sel_hi:[1,0,1]
	v_xor_b32_e32 v46, 0x80000000, v75
	v_mov_b32_e32 v47, v75
	v_pk_mul_f32 v[46:47], v[46:47], v[40:41] op_sel:[0,1] op_sel_hi:[1,0]
	s_nop 0
	v_pk_fma_f32 v[46:47], v[74:75], v[40:41], v[46:47] op_sel_hi:[0,1,1]
	ds_write_b64 v13, v[46:47] offset:54912
	v_xor_b32_e32 v46, 0x80000000, v41
	v_mov_b32_e32 v47, v41
	v_pk_mul_f32 v[46:47], v[22:23], v[46:47] op_sel:[1,0] op_sel_hi:[0,1]
	v_pk_fma_f32 v[40:41], v[22:23], v[40:41], v[46:47] op_sel_hi:[1,0,1]
	v_xor_b32_e32 v46, 0x80000000, v45
	v_mov_b32_e32 v47, v45
	v_pk_mul_f32 v[46:47], v[46:47], v[40:41] op_sel:[0,1] op_sel_hi:[1,0]
	s_nop 0
	v_pk_fma_f32 v[44:45], v[44:45], v[40:41], v[46:47] op_sel_hi:[0,1,1]
	ds_write_b64 v13, v[44:45] offset:59136
	v_xor_b32_e32 v44, 0x80000000, v41
	v_mov_b32_e32 v45, v41
	v_pk_mul_f32 v[44:45], v[22:23], v[44:45] op_sel:[1,0] op_sel_hi:[0,1]
	v_pk_fma_f32 v[40:41], v[22:23], v[40:41], v[44:45] op_sel_hi:[1,0,1]
	v_xor_b32_e32 v44, 0x80000000, v69
	v_mov_b32_e32 v45, v69
	v_pk_mul_f32 v[44:45], v[44:45], v[40:41] op_sel:[0,1] op_sel_hi:[1,0]
	s_nop 0
	v_pk_fma_f32 v[44:45], v[68:69], v[40:41], v[44:45] op_sel_hi:[0,1,1]
	ds_write_b64 v13, v[44:45] offset:63360
	v_xor_b32_e32 v44, 0x80000000, v41
	v_mov_b32_e32 v45, v41
	v_pk_mul_f32 v[44:45], v[22:23], v[44:45] op_sel:[1,0] op_sel_hi:[0,1]
	v_pk_fma_f32 v[40:41], v[22:23], v[40:41], v[44:45] op_sel_hi:[1,0,1]
	s_mov_b32 s46, s43
	v_sub_f32_e32 v10, v30, v31
	v_pk_mul_f32 v[30:31], v[40:41], s[46:47]
	s_nop 0
	v_pk_fma_f32 v[30:31], v[10:11], v[40:41], v[30:31] op_sel:[0,0,1] op_sel_hi:[0,1,0]
	v_add_u32_e32 v10, 0x10800, v13
	ds_write_b64 v10, v[30:31]
	v_xor_b32_e32 v30, 0x80000000, v41
	v_mov_b32_e32 v31, v41
	v_pk_mul_f32 v[30:31], v[22:23], v[30:31] op_sel:[1,0] op_sel_hi:[0,1]
	v_pk_fma_f32 v[30:31], v[22:23], v[40:41], v[30:31] op_sel_hi:[1,0,1]
	v_xor_b32_e32 v40, 0x80000000, v55
	v_mov_b32_e32 v41, v55
	v_pk_mul_f32 v[40:41], v[40:41], v[30:31] op_sel:[0,1] op_sel_hi:[1,0]
	v_add_u32_e32 v10, 0x11880, v13
	v_pk_fma_f32 v[40:41], v[54:55], v[30:31], v[40:41] op_sel_hi:[0,1,1]
	ds_write_b64 v10, v[40:41]
	v_xor_b32_e32 v40, 0x80000000, v31
	v_mov_b32_e32 v41, v31
	v_pk_mul_f32 v[40:41], v[22:23], v[40:41] op_sel:[1,0] op_sel_hi:[0,1]
	v_pk_fma_f32 v[30:31], v[22:23], v[30:31], v[40:41] op_sel_hi:[1,0,1]
	v_xor_b32_e32 v40, 0x80000000, v37
	v_mov_b32_e32 v41, v37
	v_pk_mul_f32 v[40:41], v[40:41], v[30:31] op_sel:[0,1] op_sel_hi:[1,0]
	v_add_u32_e32 v10, 0x12900, v13
	v_pk_fma_f32 v[36:37], v[36:37], v[30:31], v[40:41] op_sel_hi:[0,1,1]
	ds_write_b64 v10, v[36:37]
	v_xor_b32_e32 v36, 0x80000000, v31
	v_mov_b32_e32 v37, v31
	v_pk_mul_f32 v[36:37], v[22:23], v[36:37] op_sel:[1,0] op_sel_hi:[0,1]
	v_pk_fma_f32 v[30:31], v[22:23], v[30:31], v[36:37] op_sel_hi:[1,0,1]
	v_xor_b32_e32 v36, 0x80000000, v57
	v_mov_b32_e32 v37, v57
	v_pk_mul_f32 v[36:37], v[36:37], v[30:31] op_sel:[0,1] op_sel_hi:[1,0]
	v_add_u32_e32 v10, 0x13980, v13
	v_pk_fma_f32 v[36:37], v[56:57], v[30:31], v[36:37] op_sel_hi:[0,1,1]
	ds_write_b64 v10, v[36:37]
	v_xor_b32_e32 v36, 0x80000000, v31
	v_mov_b32_e32 v37, v31
	v_pk_mul_f32 v[36:37], v[22:23], v[36:37] op_sel:[1,0] op_sel_hi:[0,1]
	v_pk_fma_f32 v[30:31], v[22:23], v[30:31], v[36:37] op_sel_hi:[1,0,1]
	v_xor_b32_e32 v36, 0x80000000, v27
	v_mov_b32_e32 v37, v27
	v_pk_mul_f32 v[36:37], v[36:37], v[30:31] op_sel:[0,1] op_sel_hi:[1,0]
	v_add_u32_e32 v10, 0x14a00, v13
	v_pk_fma_f32 v[26:27], v[26:27], v[30:31], v[36:37] op_sel_hi:[0,1,1]
	ds_write_b64 v10, v[26:27]
	v_xor_b32_e32 v26, 0x80000000, v31
	v_mov_b32_e32 v27, v31
	v_pk_mul_f32 v[26:27], v[22:23], v[26:27] op_sel:[1,0] op_sel_hi:[0,1]
	v_pk_fma_f32 v[26:27], v[22:23], v[30:31], v[26:27] op_sel_hi:[1,0,1]
	v_xor_b32_e32 v30, 0x80000000, v49
	v_mov_b32_e32 v31, v49
	v_pk_mul_f32 v[30:31], v[30:31], v[26:27] op_sel:[0,1] op_sel_hi:[1,0]
	v_add_u32_e32 v10, 0x15a80, v13
	v_pk_fma_f32 v[30:31], v[48:49], v[26:27], v[30:31] op_sel_hi:[0,1,1]
	ds_write_b64 v10, v[30:31]
	v_xor_b32_e32 v30, 0x80000000, v27
	v_mov_b32_e32 v31, v27
	v_pk_mul_f32 v[30:31], v[22:23], v[30:31] op_sel:[1,0] op_sel_hi:[0,1]
	v_pk_fma_f32 v[26:27], v[22:23], v[26:27], v[30:31] op_sel_hi:[1,0,1]
	v_xor_b32_e32 v30, 0x80000000, v29
	v_mov_b32_e32 v31, v29
	v_pk_mul_f32 v[30:31], v[30:31], v[26:27] op_sel:[0,1] op_sel_hi:[1,0]
	v_add_u32_e32 v10, 0x16b00, v13
	v_pk_fma_f32 v[28:29], v[28:29], v[26:27], v[30:31] op_sel_hi:[0,1,1]
	ds_write_b64 v10, v[28:29]
	v_xor_b32_e32 v28, 0x80000000, v27
	v_mov_b32_e32 v29, v27
	v_pk_mul_f32 v[28:29], v[22:23], v[28:29] op_sel:[1,0] op_sel_hi:[0,1]
	v_pk_fma_f32 v[26:27], v[22:23], v[26:27], v[28:29] op_sel_hi:[1,0,1]
	v_xor_b32_e32 v28, 0x80000000, v53
	v_mov_b32_e32 v29, v53
	v_pk_mul_f32 v[28:29], v[28:29], v[26:27] op_sel:[0,1] op_sel_hi:[1,0]
	v_add_u32_e32 v10, 0x17b80, v13
	v_pk_fma_f32 v[28:29], v[52:53], v[26:27], v[28:29] op_sel_hi:[0,1,1]
	ds_write_b64 v10, v[28:29]
	v_xor_b32_e32 v28, 0x80000000, v27
	v_mov_b32_e32 v29, v27
	v_pk_mul_f32 v[28:29], v[22:23], v[28:29] op_sel:[1,0] op_sel_hi:[0,1]
	v_pk_fma_f32 v[26:27], v[22:23], v[26:27], v[28:29] op_sel_hi:[1,0,1]
	v_xor_b32_e32 v28, 0x80000000, v21
	v_mov_b32_e32 v29, v21
	v_pk_mul_f32 v[28:29], v[28:29], v[26:27] op_sel:[0,1] op_sel_hi:[1,0]
	v_add_u32_e32 v10, 0x18c00, v13
	v_pk_fma_f32 v[20:21], v[20:21], v[26:27], v[28:29] op_sel_hi:[0,1,1]
	ds_write_b64 v10, v[20:21]
	v_xor_b32_e32 v20, 0x80000000, v27
	v_mov_b32_e32 v21, v27
	v_pk_mul_f32 v[20:21], v[22:23], v[20:21] op_sel:[1,0] op_sel_hi:[0,1]
	v_pk_fma_f32 v[20:21], v[22:23], v[26:27], v[20:21] op_sel_hi:[1,0,1]
	v_xor_b32_e32 v26, 0x80000000, v39
	v_mov_b32_e32 v27, v39
	v_pk_mul_f32 v[26:27], v[26:27], v[20:21] op_sel:[0,1] op_sel_hi:[1,0]
	v_add_u32_e32 v10, 0x19c80, v13
	v_pk_fma_f32 v[26:27], v[38:39], v[20:21], v[26:27] op_sel_hi:[0,1,1]
	ds_write_b64 v10, v[26:27]
	v_xor_b32_e32 v26, 0x80000000, v21
	v_mov_b32_e32 v27, v21
	v_pk_mul_f32 v[26:27], v[22:23], v[26:27] op_sel:[1,0] op_sel_hi:[0,1]
	v_pk_fma_f32 v[20:21], v[22:23], v[20:21], v[26:27] op_sel_hi:[1,0,1]
	v_xor_b32_e32 v26, 0x80000000, v25
	v_mov_b32_e32 v27, v25
	v_pk_mul_f32 v[26:27], v[26:27], v[20:21] op_sel:[0,1] op_sel_hi:[1,0]
	v_add_u32_e32 v10, 0x1ad00, v13
	v_pk_fma_f32 v[24:25], v[24:25], v[20:21], v[26:27] op_sel_hi:[0,1,1]
	ds_write_b64 v10, v[24:25]
	v_xor_b32_e32 v24, 0x80000000, v21
	v_mov_b32_e32 v25, v21
	v_pk_mul_f32 v[24:25], v[22:23], v[24:25] op_sel:[1,0] op_sel_hi:[0,1]
	v_pk_fma_f32 v[20:21], v[22:23], v[20:21], v[24:25] op_sel_hi:[1,0,1]
	v_xor_b32_e32 v24, 0x80000000, v43
	v_mov_b32_e32 v25, v43
	v_pk_mul_f32 v[24:25], v[24:25], v[20:21] op_sel:[0,1] op_sel_hi:[1,0]
	v_add_u32_e32 v10, 0x1bd80, v13
	v_pk_fma_f32 v[24:25], v[42:43], v[20:21], v[24:25] op_sel_hi:[0,1,1]
	ds_write_b64 v10, v[24:25]
	v_xor_b32_e32 v24, 0x80000000, v21
	v_mov_b32_e32 v25, v21
	v_pk_mul_f32 v[24:25], v[22:23], v[24:25] op_sel:[1,0] op_sel_hi:[0,1]
	v_pk_fma_f32 v[20:21], v[22:23], v[20:21], v[24:25] op_sel_hi:[1,0,1]
	v_xor_b32_e32 v24, 0x80000000, v15
	v_mov_b32_e32 v25, v15
	v_pk_mul_f32 v[24:25], v[24:25], v[20:21] op_sel:[0,1] op_sel_hi:[1,0]
	v_add_u32_e32 v10, 0x1ce00, v13
	v_pk_fma_f32 v[14:15], v[14:15], v[20:21], v[24:25] op_sel_hi:[0,1,1]
	ds_write_b64 v10, v[14:15]
	v_xor_b32_e32 v14, 0x80000000, v21
	v_mov_b32_e32 v15, v21
	v_pk_mul_f32 v[14:15], v[22:23], v[14:15] op_sel:[1,0] op_sel_hi:[0,1]
	v_pk_fma_f32 v[14:15], v[22:23], v[20:21], v[14:15] op_sel_hi:[1,0,1]
	v_xor_b32_e32 v20, 0x80000000, v35
	v_mov_b32_e32 v21, v35
	v_pk_mul_f32 v[20:21], v[20:21], v[14:15] op_sel:[0,1] op_sel_hi:[1,0]
	v_add_u32_e32 v10, 0x1de80, v13
	v_pk_fma_f32 v[20:21], v[34:35], v[14:15], v[20:21] op_sel_hi:[0,1,1]
	ds_write_b64 v10, v[20:21]
	v_xor_b32_e32 v20, 0x80000000, v15
	v_mov_b32_e32 v21, v15
	v_pk_mul_f32 v[20:21], v[22:23], v[20:21] op_sel:[1,0] op_sel_hi:[0,1]
	v_pk_fma_f32 v[14:15], v[22:23], v[14:15], v[20:21] op_sel_hi:[1,0,1]
	v_xor_b32_e32 v20, 0x80000000, v19
	v_mov_b32_e32 v21, v19
	v_pk_mul_f32 v[20:21], v[20:21], v[14:15] op_sel:[0,1] op_sel_hi:[1,0]
	v_add_u32_e32 v10, 0x1ef00, v13
	v_pk_fma_f32 v[18:19], v[18:19], v[14:15], v[20:21] op_sel_hi:[0,1,1]
	ds_write_b64 v10, v[18:19]
	v_xor_b32_e32 v18, 0x80000000, v15
	v_mov_b32_e32 v19, v15
	v_pk_mul_f32 v[18:19], v[22:23], v[18:19] op_sel:[1,0] op_sel_hi:[0,1]
	v_pk_fma_f32 v[14:15], v[22:23], v[14:15], v[18:19] op_sel_hi:[1,0,1]
	v_xor_b32_e32 v18, 0x80000000, v33
	v_mov_b32_e32 v19, v33
	v_pk_mul_f32 v[18:19], v[18:19], v[14:15] op_sel:[0,1] op_sel_hi:[1,0]
	v_add_u32_e32 v10, 0x1ff80, v13
	v_pk_fma_f32 v[14:15], v[32:33], v[14:15], v[18:19] op_sel_hi:[0,1,1]
	ds_write_b64 v10, v[14:15]
	v_mov_b32_e32 v10, v176
	v_mov_b32_e32 v13, v173
	s_waitcnt lgkmcnt(0)
	s_barrier
	v_mov_b32_e32 v14, v182
	v_xad_u32 v30, v13, 3, v10
	v_lshl_add_u32 v73, v30, 3, 0
	v_xad_u32 v30, v13, 4, v10
	v_lshl_add_u32 v72, v30, 3, 0
	v_xad_u32 v30, v13, 5, v10
	v_lshl_add_u32 v71, v30, 3, 0
	v_xad_u32 v30, v13, 6, v10
	v_lshl_add_u32 v70, v30, 3, 0
	v_xad_u32 v30, v13, 7, v10
	v_lshl_add_u32 v69, v30, 3, 0
	v_xad_u32 v30, v13, 8, v10
	v_lshl_add_u32 v30, v30, 3, 0
	v_add_u32_e32 v68, 0x800, v30
	v_xad_u32 v30, v13, 9, v10
	v_lshl_add_u32 v30, v30, 3, 0
	v_add_u32_e32 v67, 0x800, v30
	v_xad_u32 v30, v13, 10, v10
	v_lshl_add_u32 v30, v30, 3, 0
	v_add_u32_e32 v66, 0x800, v30
	v_xad_u32 v30, v13, 11, v10
	v_lshl_add_u32 v30, v30, 3, 0
	v_add_u32_e32 v18, v13, v10
	v_add_u32_e32 v65, 0x800, v30
	v_xad_u32 v30, v13, 12, v10
	v_mov_b32_e32 v15, v183
	v_lshl_add_u32 v76, v18, 3, 0
	v_lshl_add_u32 v30, v30, 3, 0
	ds_read2_b64 v[18:21], v76 offset1:16
	ds_read2_b64 v[40:43], v68 offset1:16
	v_add_u32_e32 v64, 0x800, v30
	v_xad_u32 v30, v13, 13, v10
	v_xad_u32 v22, v13, 1, v10
	v_lshl_add_u32 v30, v30, 3, 0
	v_lshl_add_u32 v75, v22, 3, 0
	v_xad_u32 v26, v13, 2, v10
	v_add_u32_e32 v63, 0x800, v30
	v_xad_u32 v30, v13, 14, v10
	v_xad_u32 v10, v13, 15, v10
	ds_read2_b64 v[22:25], v75 offset0:32 offset1:48
	ds_read2_b64 v[48:51], v67 offset0:32 offset1:48
	v_lshl_add_u32 v30, v30, 3, 0
	v_lshl_add_u32 v10, v10, 3, 0
	v_lshl_add_u32 v74, v26, 3, 0
	v_add_u32_e32 v62, 0x800, v30
	v_add_u32_e32 v13, 0x800, v10
	v_mov_b32_e32 v10, v164
	ds_read2_b64 v[26:29], v74 offset0:64 offset1:80
	ds_read2_b64 v[58:61], v73 offset0:96 offset1:112
	ds_read2_b64 v[78:81], v72 offset0:128 offset1:144
	ds_read2_b64 v[82:85], v71 offset0:160 offset1:176
	ds_read2_b64 v[86:89], v70 offset0:192 offset1:208
	ds_read2_b64 v[90:93], v69 offset0:224 offset1:240
	ds_read2_b64 v[54:57], v66 offset0:64 offset1:80
	ds_read2_b64 v[94:97], v65 offset0:96 offset1:112
	ds_read2_b64 v[98:101], v64 offset0:128 offset1:144
	ds_read2_b64 v[102:105], v63 offset0:160 offset1:176
	ds_read2_b64 v[106:109], v62 offset0:192 offset1:208
	ds_read2_b64 v[110:113], v13 offset0:224 offset1:240
	s_waitcnt lgkmcnt(14)
	v_pk_add_f32 v[114:115], v[18:19], v[40:41]
	v_pk_add_f32 v[40:41], v[18:19], v[40:41] neg_lo:[0,1] neg_hi:[0,1]
	v_pk_add_f32 v[18:19], v[20:21], v[42:43]
	v_pk_add_f32 v[20:21], v[20:21], v[42:43] neg_lo:[0,1] neg_hi:[0,1]
	v_mov_b32_e32 v30, v165
	v_mov_b32_e32 v32, v166
	v_mov_b32_e32 v34, v167
	v_mov_b32_e32 v10, v168
	v_mov_b32_e32 v38, v169
	v_mov_b32_e32 v36, v170
	v_mov_b32_e32 v46, v171
	v_xor_b32_e32 v42, 0x80000000, v21
	v_mov_b32_e32 v43, v20
	v_mov_b32_e32 v31, v172
	v_pk_mul_f32 v[42:43], v[42:43], v[46:47] op_sel_hi:[1,0] neg_lo:[0,1] neg_hi:[0,1]
	s_mov_b32 s14, s43
	v_pk_fma_f32 v[44:45], v[20:21], v[30:31], v[42:43] op_sel_hi:[1,0,1]
	s_waitcnt lgkmcnt(12)
	v_pk_add_f32 v[20:21], v[22:23], v[48:49]
	v_pk_add_f32 v[22:23], v[22:23], v[48:49] neg_lo:[0,1] neg_hi:[0,1]
	s_mov_b32 s15, s42
	v_xor_b32_e32 v42, 0x80000000, v23
	v_mov_b32_e32 v43, v22
	v_pk_mul_f32 v[42:43], v[42:43], v[36:37] op_sel_hi:[1,0] neg_lo:[0,1] neg_hi:[0,1]
	s_nop 0
	v_pk_fma_f32 v[48:49], v[22:23], v[32:33], v[42:43] op_sel_hi:[1,0,1]
	v_pk_add_f32 v[22:23], v[24:25], v[50:51]
	v_pk_add_f32 v[24:25], v[24:25], v[50:51] neg_lo:[0,1] neg_hi:[0,1]
	s_nop 0
	v_xor_b32_e32 v42, 0x80000000, v25
	v_mov_b32_e32 v43, v24
	v_pk_mul_f32 v[42:43], v[42:43], v[38:39] op_sel_hi:[1,0] neg_lo:[0,1] neg_hi:[0,1]
	s_nop 0
	v_pk_fma_f32 v[52:53], v[24:25], v[34:35], v[42:43] op_sel_hi:[1,0,1]
	s_waitcnt lgkmcnt(5)
	v_pk_add_f32 v[24:25], v[26:27], v[54:55]
	v_pk_add_f32 v[26:27], v[26:27], v[54:55] neg_lo:[0,1] neg_hi:[0,1]
	s_nop 0
	v_xor_b32_e32 v42, 0x80000000, v27
	v_mov_b32_e32 v43, v26
	v_pk_mul_f32 v[42:43], v[42:43], v[10:11] op_sel_hi:[1,0] neg_lo:[0,1] neg_hi:[0,1]
	s_nop 0
	v_pk_fma_f32 v[54:55], v[26:27], v[10:11], v[42:43] op_sel_hi:[1,0,1]
	v_pk_add_f32 v[26:27], v[28:29], v[56:57]
	v_pk_add_f32 v[28:29], v[28:29], v[56:57] neg_lo:[0,1] neg_hi:[0,1]
	s_nop 0
	v_pk_mul_f32 v[42:43], v[28:29], v[38:39] op_sel_hi:[1,0]
	v_xor_b32_e32 v50, 0x80000000, v29
	v_mov_b32_e32 v51, v28
	v_pk_fma_f32 v[56:57], v[50:51], v[34:35], v[42:43] op_sel_hi:[1,0,1] neg_lo:[0,1,0] neg_hi:[0,1,0]
	s_waitcnt lgkmcnt(4)
	v_pk_add_f32 v[42:43], v[58:59], v[94:95] neg_lo:[0,1] neg_hi:[0,1]
	v_pk_add_f32 v[28:29], v[58:59], v[94:95]
	v_pk_mul_f32 v[50:51], v[42:43], v[36:37] op_sel_hi:[1,0]
	v_xor_b32_e32 v58, 0x80000000, v43
	v_mov_b32_e32 v59, v42
	v_pk_fma_f32 v[58:59], v[58:59], v[32:33], v[50:51] op_sel_hi:[1,0,1] neg_lo:[0,1,0] neg_hi:[0,1,0]
	v_pk_add_f32 v[50:51], v[60:61], v[96:97] neg_lo:[0,1] neg_hi:[0,1]
	v_pk_add_f32 v[42:43], v[60:61], v[96:97]
	v_pk_mul_f32 v[60:61], v[50:51], v[46:47] op_sel_hi:[1,0]
	v_xor_b32_e32 v94, 0x80000000, v51
	v_mov_b32_e32 v95, v50
	s_waitcnt lgkmcnt(3)
	v_pk_add_f32 v[50:51], v[78:79], v[98:99]
	v_pk_add_f32 v[78:79], v[78:79], v[98:99] neg_lo:[0,1] neg_hi:[0,1]
	v_pk_fma_f32 v[60:61], v[94:95], v[30:31], v[60:61] op_sel_hi:[1,0,1] neg_lo:[0,1,0] neg_hi:[0,1,0]
	v_xor_b32_e32 v95, 0x80000000, v78
	v_mov_b32_e32 v94, v79
	v_pk_add_f32 v[78:79], v[80:81], v[100:101]
	v_pk_add_f32 v[80:81], v[80:81], v[100:101] neg_lo:[0,1] neg_hi:[0,1]
	s_nop 0
	v_pk_mul_f32 v[96:97], v[80:81], v[46:47] op_sel_hi:[1,0] neg_lo:[0,1] neg_hi:[0,1]
	v_xor_b32_e32 v98, 0x80000000, v81
	v_mov_b32_e32 v99, v80
	v_pk_fma_f32 v[80:81], v[98:99], v[30:31], v[96:97] op_sel_hi:[1,0,1] neg_lo:[0,1,0] neg_hi:[0,1,0]
	s_waitcnt lgkmcnt(2)
	v_pk_add_f32 v[96:97], v[82:83], v[102:103]
	v_pk_add_f32 v[82:83], v[82:83], v[102:103] neg_lo:[0,1] neg_hi:[0,1]
	s_nop 0
	v_pk_mul_f32 v[98:99], v[82:83], v[36:37] op_sel_hi:[1,0] neg_lo:[0,1] neg_hi:[0,1]
	v_xor_b32_e32 v100, 0x80000000, v83
	v_mov_b32_e32 v101, v82
	v_pk_fma_f32 v[82:83], v[100:101], v[32:33], v[98:99] op_sel_hi:[1,0,1] neg_lo:[0,1,0] neg_hi:[0,1,0]
	v_pk_add_f32 v[98:99], v[84:85], v[104:105]
	v_pk_add_f32 v[84:85], v[84:85], v[104:105] neg_lo:[0,1] neg_hi:[0,1]
	s_nop 0
	v_pk_mul_f32 v[100:101], v[84:85], v[38:39] op_sel_hi:[1,0] neg_lo:[0,1] neg_hi:[0,1]
	v_xor_b32_e32 v102, 0x80000000, v85
	v_mov_b32_e32 v103, v84
	v_pk_fma_f32 v[84:85], v[102:103], v[34:35], v[100:101] op_sel_hi:[1,0,1] neg_lo:[0,1,0] neg_hi:[0,1,0]
	s_waitcnt lgkmcnt(1)
	v_pk_add_f32 v[100:101], v[86:87], v[106:107]
	v_pk_add_f32 v[86:87], v[86:87], v[106:107] neg_lo:[0,1] neg_hi:[0,1]
	s_nop 0
	v_xor_b32_e32 v102, 0x80000000, v87
	v_mov_b32_e32 v103, v86
	v_pk_mul_f32 v[102:103], v[102:103], v[10:11] op_sel_hi:[1,0] neg_lo:[0,1] neg_hi:[0,1]
	s_nop 0
	v_pk_fma_f32 v[86:87], v[86:87], v[10:11], v[102:103] op_sel_hi:[1,0,1] neg_lo:[0,1,0] neg_hi:[0,1,0]
	v_pk_add_f32 v[102:103], v[88:89], v[108:109]
	v_pk_add_f32 v[88:89], v[88:89], v[108:109] neg_lo:[0,1] neg_hi:[0,1]
	s_nop 0
	v_xor_b32_e32 v104, 0x80000000, v89
	v_mov_b32_e32 v105, v88
	v_pk_mul_f32 v[38:39], v[104:105], v[38:39] op_sel_hi:[1,0] neg_lo:[0,1] neg_hi:[0,1]
	s_nop 0
	v_pk_fma_f32 v[88:89], v[88:89], v[34:35], v[38:39] op_sel_hi:[1,0,1] neg_lo:[0,1,0] neg_hi:[0,1,0]
	s_waitcnt lgkmcnt(0)
	v_pk_add_f32 v[38:39], v[90:91], v[110:111] neg_lo:[0,1] neg_hi:[0,1]
	v_pk_add_f32 v[34:35], v[90:91], v[110:111]
	v_xor_b32_e32 v90, 0x80000000, v39
	v_mov_b32_e32 v91, v38
	v_pk_mul_f32 v[90:91], v[90:91], v[36:37] op_sel_hi:[1,0] neg_lo:[0,1] neg_hi:[0,1]
	s_nop 0
	v_pk_fma_f32 v[90:91], v[38:39], v[32:33], v[90:91] op_sel_hi:[1,0,1] neg_lo:[0,1,0] neg_hi:[0,1,0]
	v_pk_add_f32 v[38:39], v[92:93], v[112:113]
	v_pk_add_f32 v[92:93], v[92:93], v[112:113] neg_lo:[0,1] neg_hi:[0,1]
	s_nop 0
	v_xor_b32_e32 v104, 0x80000000, v93
	v_mov_b32_e32 v105, v92
	v_pk_mul_f32 v[46:47], v[104:105], v[46:47] op_sel_hi:[1,0] neg_lo:[0,1] neg_hi:[0,1]
	s_nop 0
	v_pk_fma_f32 v[92:93], v[92:93], v[30:31], v[46:47] op_sel_hi:[1,0,1] neg_lo:[0,1,0] neg_hi:[0,1,0]
	v_pk_add_f32 v[46:47], v[18:19], v[78:79]
	v_pk_add_f32 v[18:19], v[18:19], v[78:79] neg_lo:[0,1] neg_hi:[0,1]
	v_pk_add_f32 v[30:31], v[114:115], v[50:51]
	v_xor_b32_e32 v78, 0x80000000, v19
	v_mov_b32_e32 v79, v18
	v_pk_mul_f32 v[78:79], v[78:79], v[36:37] op_sel_hi:[1,0] neg_lo:[0,1] neg_hi:[0,1]
	v_pk_add_f32 v[50:51], v[114:115], v[50:51] neg_lo:[0,1] neg_hi:[0,1]
	v_pk_fma_f32 v[78:79], v[18:19], v[32:33], v[78:79] op_sel_hi:[1,0,1]
	v_pk_add_f32 v[18:19], v[20:21], v[96:97]
	v_pk_add_f32 v[20:21], v[20:21], v[96:97] neg_lo:[0,1] neg_hi:[0,1]
	s_nop 0
	v_xor_b32_e32 v96, 0x80000000, v21
	v_mov_b32_e32 v97, v20
	v_pk_mul_f32 v[96:97], v[96:97], v[10:11] op_sel_hi:[1,0] neg_lo:[0,1] neg_hi:[0,1]
	s_nop 0
	v_pk_fma_f32 v[20:21], v[20:21], v[10:11], v[96:97] op_sel_hi:[1,0,1]
	v_pk_add_f32 v[96:97], v[22:23], v[98:99]
	v_pk_add_f32 v[22:23], v[22:23], v[98:99] neg_lo:[0,1] neg_hi:[0,1]
	s_nop 0
	v_pk_mul_f32 v[98:99], v[22:23], v[36:37] op_sel_hi:[1,0]
	v_xor_b32_e32 v104, 0x80000000, v23
	v_mov_b32_e32 v105, v22
	v_pk_add_f32 v[22:23], v[24:25], v[100:101]
	v_pk_add_f32 v[24:25], v[24:25], v[100:101] neg_lo:[0,1] neg_hi:[0,1]
	v_pk_fma_f32 v[98:99], v[104:105], v[32:33], v[98:99] op_sel_hi:[1,0,1] neg_lo:[0,1,0] neg_hi:[0,1,0]
	v_xor_b32_e32 v101, 0x80000000, v24
	v_mov_b32_e32 v100, v25
	v_pk_add_f32 v[24:25], v[26:27], v[102:103]
	v_pk_add_f32 v[26:27], v[26:27], v[102:103] neg_lo:[0,1] neg_hi:[0,1]
	s_nop 0
	v_pk_mul_f32 v[102:103], v[26:27], v[36:37] op_sel_hi:[1,0] neg_lo:[0,1] neg_hi:[0,1]
	v_xor_b32_e32 v104, 0x80000000, v27
	v_mov_b32_e32 v105, v26
	v_pk_add_f32 v[26:27], v[28:29], v[34:35]
	v_pk_add_f32 v[28:29], v[28:29], v[34:35] neg_lo:[0,1] neg_hi:[0,1]
	v_pk_fma_f32 v[102:103], v[104:105], v[32:33], v[102:103] op_sel_hi:[1,0,1] neg_lo:[0,1,0] neg_hi:[0,1,0]
	v_xor_b32_e32 v34, 0x80000000, v29
	v_mov_b32_e32 v35, v28
	v_pk_mul_f32 v[34:35], v[34:35], v[10:11] op_sel_hi:[1,0] neg_lo:[0,1] neg_hi:[0,1]
	v_pk_add_f32 v[104:105], v[30:31], v[22:23] neg_lo:[0,1] neg_hi:[0,1]
	v_pk_fma_f32 v[28:29], v[28:29], v[10:11], v[34:35] op_sel_hi:[1,0,1] neg_lo:[0,1,0] neg_hi:[0,1,0]
	v_pk_add_f32 v[34:35], v[42:43], v[38:39]
	v_pk_add_f32 v[38:39], v[42:43], v[38:39] neg_lo:[0,1] neg_hi:[0,1]
	s_nop 0
	v_xor_b32_e32 v42, 0x80000000, v39
	v_mov_b32_e32 v43, v38
	v_pk_mul_f32 v[42:43], v[42:43], v[36:37] op_sel_hi:[1,0] neg_lo:[0,1] neg_hi:[0,1]
	s_nop 0
	v_pk_fma_f32 v[42:43], v[38:39], v[32:33], v[42:43] op_sel_hi:[1,0,1] neg_lo:[0,1,0] neg_hi:[0,1,0]
	v_pk_add_f32 v[38:39], v[30:31], v[22:23]
	v_pk_add_f32 v[22:23], v[46:47], v[24:25]
	v_pk_add_f32 v[24:25], v[46:47], v[24:25] neg_lo:[0,1] neg_hi:[0,1]
	s_nop 0
	v_xor_b32_e32 v30, 0x80000000, v25
	v_mov_b32_e32 v31, v24
	v_pk_mul_f32 v[30:31], v[30:31], v[10:11] op_sel_hi:[1,0] neg_lo:[0,1] neg_hi:[0,1]
	s_nop 0
	v_pk_fma_f32 v[24:25], v[24:25], v[10:11], v[30:31] op_sel_hi:[1,0,1]
	v_pk_add_f32 v[30:31], v[18:19], v[26:27]
	v_pk_add_f32 v[18:19], v[18:19], v[26:27] neg_lo:[0,1] neg_hi:[0,1]
	s_nop 0
	v_xor_b32_e32 v27, 0x80000000, v18
	v_mov_b32_e32 v26, v19
	v_pk_add_f32 v[18:19], v[96:97], v[34:35]
	v_pk_add_f32 v[34:35], v[96:97], v[34:35] neg_lo:[0,1] neg_hi:[0,1]
	s_nop 0
	v_xor_b32_e32 v46, 0x80000000, v35
	v_mov_b32_e32 v47, v34
	v_pk_mul_f32 v[46:47], v[46:47], v[10:11] op_sel_hi:[1,0] neg_lo:[0,1] neg_hi:[0,1]
	s_nop 0
	v_pk_fma_f32 v[34:35], v[34:35], v[10:11], v[46:47] op_sel_hi:[1,0,1] neg_lo:[0,1,0] neg_hi:[0,1,0]
	v_pk_add_f32 v[46:47], v[38:39], v[30:31]
	v_pk_add_f32 v[38:39], v[38:39], v[30:31] neg_lo:[0,1] neg_hi:[0,1]
	v_pk_add_f32 v[30:31], v[22:23], v[18:19]
	v_pk_add_f32 v[18:19], v[22:23], v[18:19] neg_lo:[0,1] neg_hi:[0,1]
	v_pk_add_f32 v[96:97], v[46:47], v[30:31]
	v_xor_b32_e32 v23, 0x80000000, v18
	v_mov_b32_e32 v22, v19
	v_pk_add_f32 v[18:19], v[104:105], v[26:27]
	v_pk_add_f32 v[104:105], v[104:105], v[26:27] neg_lo:[0,1] neg_hi:[0,1]
	v_pk_add_f32 v[26:27], v[24:25], v[34:35]
	v_pk_add_f32 v[24:25], v[24:25], v[34:35] neg_lo:[0,1] neg_hi:[0,1]
	v_pk_add_f32 v[30:31], v[46:47], v[30:31] neg_lo:[0,1] neg_hi:[0,1]
	v_xor_b32_e32 v35, 0x80000000, v24
	v_mov_b32_e32 v34, v25
	v_pk_add_f32 v[24:25], v[50:51], v[100:101]
	v_pk_add_f32 v[100:101], v[50:51], v[100:101] neg_lo:[0,1] neg_hi:[0,1]
	v_pk_add_f32 v[50:51], v[78:79], v[102:103] neg_lo:[0,1] neg_hi:[0,1]
	v_pk_add_f32 v[46:47], v[38:39], v[22:23]
	v_pk_add_f32 v[22:23], v[38:39], v[22:23] neg_lo:[0,1] neg_hi:[0,1]
	v_pk_add_f32 v[106:107], v[18:19], v[26:27]
	v_pk_add_f32 v[26:27], v[18:19], v[26:27] neg_lo:[0,1] neg_hi:[0,1]
	v_pk_add_f32 v[38:39], v[104:105], v[34:35]
	v_pk_add_f32 v[18:19], v[104:105], v[34:35] neg_lo:[0,1] neg_hi:[0,1]
	v_pk_add_f32 v[34:35], v[78:79], v[102:103]
	v_xor_b32_e32 v78, 0x80000000, v51
	v_mov_b32_e32 v79, v50
	v_pk_mul_f32 v[78:79], v[10:11], v[78:79] op_sel_hi:[0,1] neg_lo:[1,0] neg_hi:[1,0]
	v_pk_fma_f32 v[78:79], v[10:11], v[50:51], v[78:79] op_sel_hi:[0,1,1]
	v_pk_add_f32 v[50:51], v[20:21], v[28:29]
	v_pk_add_f32 v[20:21], v[20:21], v[28:29] neg_lo:[0,1] neg_hi:[0,1]
	s_nop 0
	v_xor_b32_e32 v29, 0x80000000, v20
	v_mov_b32_e32 v28, v21
	v_pk_add_f32 v[20:21], v[98:99], v[42:43]
	v_pk_add_f32 v[42:43], v[98:99], v[42:43] neg_lo:[0,1] neg_hi:[0,1]
	s_nop 0
	v_xor_b32_e32 v98, 0x80000000, v43
	v_mov_b32_e32 v99, v42
	v_pk_mul_f32 v[98:99], v[10:11], v[98:99] op_sel_hi:[0,1] neg_lo:[1,0] neg_hi:[1,0]
	v_pk_fma_f32 v[42:43], v[10:11], v[42:43], v[98:99] op_sel_hi:[0,1,1] neg_lo:[1,0,0] neg_hi:[1,0,0]
	v_pk_add_f32 v[98:99], v[24:25], v[50:51]
	v_pk_add_f32 v[24:25], v[24:25], v[50:51] neg_lo:[0,1] neg_hi:[0,1]
	v_pk_add_f32 v[50:51], v[34:35], v[20:21]
	v_pk_add_f32 v[20:21], v[34:35], v[20:21] neg_lo:[0,1] neg_hi:[0,1]
	v_pk_add_f32 v[104:105], v[98:99], v[50:51]
	v_xor_b32_e32 v103, 0x80000000, v20
	v_mov_b32_e32 v102, v21
	v_pk_add_f32 v[34:35], v[98:99], v[50:51] neg_lo:[0,1] neg_hi:[0,1]
	v_pk_add_f32 v[20:21], v[100:101], v[28:29]
	v_pk_add_f32 v[98:99], v[100:101], v[28:29] neg_lo:[0,1] neg_hi:[0,1]
	v_pk_add_f32 v[28:29], v[78:79], v[42:43]
	v_pk_add_f32 v[42:43], v[78:79], v[42:43] neg_lo:[0,1] neg_hi:[0,1]
	v_pk_add_f32 v[100:101], v[20:21], v[28:29]
	v_xor_b32_e32 v79, 0x80000000, v42
	v_mov_b32_e32 v78, v43
	v_pk_add_f32 v[28:29], v[20:21], v[28:29] neg_lo:[0,1] neg_hi:[0,1]
	v_pk_add_f32 v[42:43], v[98:99], v[78:79]
	v_pk_add_f32 v[20:21], v[98:99], v[78:79] neg_lo:[0,1] neg_hi:[0,1]
	v_pk_add_f32 v[78:79], v[40:41], v[94:95]
	v_pk_add_f32 v[94:95], v[40:41], v[94:95] neg_lo:[0,1] neg_hi:[0,1]
	v_pk_add_f32 v[40:41], v[44:45], v[80:81]
	v_pk_add_f32 v[44:45], v[44:45], v[80:81] neg_lo:[0,1] neg_hi:[0,1]
	v_pk_add_f32 v[50:51], v[24:25], v[102:103]
	v_xor_b32_e32 v80, 0x80000000, v45
	v_mov_b32_e32 v81, v44
	v_pk_mul_f32 v[80:81], v[36:37], v[80:81] op_sel_hi:[0,1] neg_lo:[1,0] neg_hi:[1,0]
	v_pk_fma_f32 v[44:45], v[32:33], v[44:45], v[80:81] op_sel_hi:[0,1,1]
	v_pk_add_f32 v[80:81], v[48:49], v[82:83]
	v_pk_add_f32 v[48:49], v[48:49], v[82:83] neg_lo:[0,1] neg_hi:[0,1]
	v_pk_add_f32 v[24:25], v[24:25], v[102:103] neg_lo:[0,1] neg_hi:[0,1]
	v_xor_b32_e32 v82, 0x80000000, v49
	v_mov_b32_e32 v83, v48
	v_pk_mul_f32 v[82:83], v[10:11], v[82:83] op_sel_hi:[0,1] neg_lo:[1,0] neg_hi:[1,0]
	v_pk_fma_f32 v[82:83], v[10:11], v[48:49], v[82:83] op_sel_hi:[0,1,1]
	v_pk_add_f32 v[48:49], v[52:53], v[84:85]
	v_pk_add_f32 v[52:53], v[52:53], v[84:85] neg_lo:[0,1] neg_hi:[0,1]
	s_nop 0
	v_xor_b32_e32 v84, 0x80000000, v53
	v_mov_b32_e32 v85, v52
	v_pk_mul_f32 v[84:85], v[32:33], v[84:85] op_sel_hi:[0,1] neg_lo:[1,0] neg_hi:[1,0]
	v_pk_fma_f32 v[52:53], v[36:37], v[52:53], v[84:85] op_sel_hi:[0,1,1]
	v_pk_add_f32 v[84:85], v[54:55], v[86:87]
	v_pk_add_f32 v[54:55], v[54:55], v[86:87] neg_lo:[0,1] neg_hi:[0,1]
	s_nop 0
	v_xor_b32_e32 v87, 0x80000000, v54
	v_mov_b32_e32 v86, v55
	v_pk_add_f32 v[54:55], v[56:57], v[88:89]
	v_pk_add_f32 v[56:57], v[56:57], v[88:89] neg_lo:[0,1] neg_hi:[0,1]
	s_nop 0
	v_xor_b32_e32 v88, 0x80000000, v57
	v_mov_b32_e32 v89, v56
	v_pk_mul_f32 v[88:89], v[32:33], v[88:89] op_sel_hi:[0,1] neg_lo:[1,0] neg_hi:[1,0]
	v_pk_fma_f32 v[56:57], v[36:37], v[56:57], v[88:89] op_sel_hi:[0,1,1] neg_lo:[1,0,0] neg_hi:[1,0,0]
	v_pk_add_f32 v[88:89], v[58:59], v[90:91]
	v_pk_add_f32 v[58:59], v[58:59], v[90:91] neg_lo:[0,1] neg_hi:[0,1]
	s_nop 0
	v_xor_b32_e32 v90, 0x80000000, v59
	v_mov_b32_e32 v91, v58
	v_pk_mul_f32 v[90:91], v[10:11], v[90:91] op_sel_hi:[0,1] neg_lo:[1,0] neg_hi:[1,0]
	v_pk_fma_f32 v[58:59], v[10:11], v[58:59], v[90:91] op_sel_hi:[0,1,1] neg_lo:[1,0,0] neg_hi:[1,0,0]
	v_pk_add_f32 v[90:91], v[60:61], v[92:93]
	v_pk_add_f32 v[60:61], v[60:61], v[92:93] neg_lo:[0,1] neg_hi:[0,1]
	s_nop 0
	v_xor_b32_e32 v92, 0x80000000, v61
	v_mov_b32_e32 v93, v60
	v_pk_mul_f32 v[36:37], v[36:37], v[92:93] op_sel_hi:[0,1] neg_lo:[1,0] neg_hi:[1,0]
	v_pk_fma_f32 v[36:37], v[32:33], v[60:61], v[36:37] op_sel_hi:[0,1,1] neg_lo:[1,0,0] neg_hi:[1,0,0]
	v_pk_add_f32 v[32:33], v[78:79], v[84:85]
	v_pk_add_f32 v[60:61], v[78:79], v[84:85] neg_lo:[0,1] neg_hi:[0,1]
	v_pk_add_f32 v[78:79], v[54:55], v[40:41]
	v_pk_add_f32 v[40:41], v[40:41], v[54:55] neg_lo:[0,1] neg_hi:[0,1]
	s_nop 0
	v_xor_b32_e32 v54, 0x80000000, v41
	v_mov_b32_e32 v55, v40
	v_pk_mul_f32 v[54:55], v[10:11], v[54:55] op_sel_hi:[0,1] neg_lo:[1,0] neg_hi:[1,0]
	v_pk_fma_f32 v[54:55], v[10:11], v[40:41], v[54:55] op_sel_hi:[0,1,1]
	v_pk_add_f32 v[40:41], v[80:81], v[88:89]
	v_pk_add_f32 v[80:81], v[80:81], v[88:89] neg_lo:[0,1] neg_hi:[0,1]
	s_nop 0
	v_xor_b32_e32 v85, 0x80000000, v80
	v_mov_b32_e32 v84, v81
	v_pk_add_f32 v[80:81], v[48:49], v[90:91]
	v_pk_add_f32 v[48:49], v[48:49], v[90:91] neg_lo:[0,1] neg_hi:[0,1]
	v_pk_add_f32 v[90:91], v[78:79], v[80:81]
	v_xor_b32_e32 v88, 0x80000000, v49
	v_mov_b32_e32 v89, v48
	v_pk_mul_f32 v[88:89], v[10:11], v[88:89] op_sel_hi:[0,1] neg_lo:[1,0] neg_hi:[1,0]
	v_pk_fma_f32 v[48:49], v[10:11], v[48:49], v[88:89] op_sel_hi:[0,1,1] neg_lo:[1,0,0] neg_hi:[1,0,0]
	v_pk_add_f32 v[88:89], v[32:33], v[40:41]
	v_pk_add_f32 v[32:33], v[32:33], v[40:41] neg_lo:[0,1] neg_hi:[0,1]
	v_pk_add_f32 v[40:41], v[78:79], v[80:81] neg_lo:[0,1] neg_hi:[0,1]
	v_pk_add_f32 v[80:81], v[88:89], v[90:91] neg_lo:[0,1] neg_hi:[0,1]
	v_xor_b32_e32 v79, 0x80000000, v40
	v_mov_b32_e32 v78, v41
	v_pk_add_f32 v[92:93], v[32:33], v[78:79]
	v_pk_add_f32 v[40:41], v[32:33], v[78:79] neg_lo:[0,1] neg_hi:[0,1]
	v_pk_add_f32 v[78:79], v[54:55], v[48:49]
	v_pk_add_f32 v[48:49], v[54:55], v[48:49] neg_lo:[0,1] neg_hi:[0,1]
	v_pk_add_f32 v[32:33], v[60:61], v[84:85]
	v_pk_add_f32 v[60:61], v[60:61], v[84:85] neg_lo:[0,1] neg_hi:[0,1]
	v_xor_b32_e32 v55, 0x80000000, v48
	v_mov_b32_e32 v54, v49
	v_pk_add_f32 v[84:85], v[32:33], v[78:79]
	v_pk_add_f32 v[48:49], v[32:33], v[78:79] neg_lo:[0,1] neg_hi:[0,1]
	v_pk_add_f32 v[78:79], v[60:61], v[54:55]
	v_pk_add_f32 v[32:33], v[60:61], v[54:55] neg_lo:[0,1] neg_hi:[0,1]
	v_pk_add_f32 v[54:55], v[94:95], v[86:87]
	v_pk_add_f32 v[60:61], v[94:95], v[86:87] neg_lo:[0,1] neg_hi:[0,1]
	v_pk_add_f32 v[86:87], v[56:57], v[44:45]
	v_pk_add_f32 v[44:45], v[44:45], v[56:57] neg_lo:[0,1] neg_hi:[0,1]
	v_pk_add_f32 v[88:89], v[88:89], v[90:91]
	v_xor_b32_e32 v56, 0x80000000, v45
	v_mov_b32_e32 v57, v44
	v_pk_mul_f32 v[56:57], v[10:11], v[56:57] op_sel_hi:[0,1] neg_lo:[1,0] neg_hi:[1,0]
	v_pk_fma_f32 v[56:57], v[10:11], v[44:45], v[56:57] op_sel_hi:[0,1,1]
	v_pk_add_f32 v[44:45], v[82:83], v[58:59]
	v_pk_add_f32 v[58:59], v[82:83], v[58:59] neg_lo:[0,1] neg_hi:[0,1]
	v_xor_b32_e32 v90, 0x80000000, v89
	v_xor_b32_e32 v83, 0x80000000, v58
	v_mov_b32_e32 v82, v59
	v_pk_add_f32 v[58:59], v[52:53], v[36:37]
	v_pk_add_f32 v[36:37], v[52:53], v[36:37] neg_lo:[0,1] neg_hi:[0,1]
	v_mov_b32_e32 v91, v89
	v_xor_b32_e32 v52, 0x80000000, v37
	v_mov_b32_e32 v53, v36
	v_pk_mul_f32 v[52:53], v[10:11], v[52:53] op_sel_hi:[0,1] neg_lo:[1,0] neg_hi:[1,0]
	v_pk_fma_f32 v[36:37], v[10:11], v[36:37], v[52:53] op_sel_hi:[0,1,1] neg_lo:[1,0,0] neg_hi:[1,0,0]
	v_pk_add_f32 v[52:53], v[54:55], v[44:45]
	v_pk_add_f32 v[44:45], v[54:55], v[44:45] neg_lo:[0,1] neg_hi:[0,1]
	v_pk_add_f32 v[54:55], v[86:87], v[58:59]
	v_pk_add_f32 v[58:59], v[86:87], v[58:59] neg_lo:[0,1] neg_hi:[0,1]
	s_nop 0
	v_xor_b32_e32 v87, 0x80000000, v58
	v_mov_b32_e32 v86, v59
	v_pk_add_f32 v[58:59], v[52:53], v[54:55]
	v_pk_add_f32 v[54:55], v[52:53], v[54:55] neg_lo:[0,1] neg_hi:[0,1]
	v_pk_add_f32 v[52:53], v[60:61], v[82:83]
	v_pk_add_f32 v[60:61], v[60:61], v[82:83] neg_lo:[0,1] neg_hi:[0,1]
	v_pk_add_f32 v[82:83], v[56:57], v[36:37]
	v_pk_add_f32 v[36:37], v[56:57], v[36:37] neg_lo:[0,1] neg_hi:[0,1]
	v_pk_add_f32 v[94:95], v[44:45], v[86:87]
	v_xor_b32_e32 v57, 0x80000000, v36
	v_mov_b32_e32 v56, v37
	v_pk_add_f32 v[44:45], v[44:45], v[86:87] neg_lo:[0,1] neg_hi:[0,1]
	v_pk_add_f32 v[86:87], v[52:53], v[82:83]
	v_pk_add_f32 v[52:53], v[52:53], v[82:83] neg_lo:[0,1] neg_hi:[0,1]
	v_pk_add_f32 v[82:83], v[60:61], v[56:57]
	v_pk_add_f32 v[36:37], v[60:61], v[56:57] neg_lo:[0,1] neg_hi:[0,1]
	v_xor_b32_e32 v56, 0x80000000, v97
	v_mov_b32_e32 v57, v97
	v_pk_fma_f32 v[60:61], v[14:15], s[92:93], v[14:15] op_sel:[1,0,0] op_sel_hi:[0,1,1]
	v_pk_mul_f32 v[56:57], v[56:57], s[14:15]
	v_pk_mul_f32 v[90:91], v[60:61], v[90:91] op_sel:[1,0] op_sel_hi:[0,1]
	v_pk_fma_f32 v[56:57], v[96:97], s[42:43], v[56:57] op_sel_hi:[0,1,1]
	v_pk_fma_f32 v[88:89], v[60:61], v[88:89], v[90:91] op_sel_hi:[1,0,1]
	ds_write2_b64 v76, v[56:57], v[88:89] offset1:16
	v_xor_b32_e32 v56, 0x80000000, v61
	v_mov_b32_e32 v57, v61
	v_pk_mul_f32 v[56:57], v[14:15], v[56:57] op_sel:[1,0] op_sel_hi:[0,1]
	v_pk_fma_f32 v[56:57], v[14:15], v[60:61], v[56:57] op_sel_hi:[1,0,1]
	v_xor_b32_e32 v60, 0x80000000, v105
	v_mov_b32_e32 v61, v105
	v_xor_b32_e32 v76, 0x80000000, v57
	v_mov_b32_e32 v77, v57
	v_pk_mul_f32 v[60:61], v[56:57], v[60:61] op_sel:[1,0] op_sel_hi:[0,1]
	v_pk_mul_f32 v[76:77], v[14:15], v[76:77] op_sel:[1,0] op_sel_hi:[0,1]
	v_pk_fma_f32 v[60:61], v[56:57], v[104:105], v[60:61] op_sel_hi:[1,0,1]
	v_pk_fma_f32 v[56:57], v[14:15], v[56:57], v[76:77] op_sel_hi:[1,0,1]
	v_xor_b32_e32 v76, 0x80000000, v59
	v_mov_b32_e32 v77, v59
	v_pk_mul_f32 v[76:77], v[56:57], v[76:77] op_sel:[1,0] op_sel_hi:[0,1]
	v_pk_fma_f32 v[58:59], v[56:57], v[58:59], v[76:77] op_sel_hi:[1,0,1]
	ds_write2_b64 v75, v[60:61], v[58:59] offset0:32 offset1:48
	v_xor_b32_e32 v58, 0x80000000, v57
	v_mov_b32_e32 v59, v57
	v_pk_mul_f32 v[58:59], v[14:15], v[58:59] op_sel:[1,0] op_sel_hi:[0,1]
	v_pk_fma_f32 v[56:57], v[14:15], v[56:57], v[58:59] op_sel_hi:[1,0,1]
	v_xor_b32_e32 v58, 0x80000000, v107
	v_mov_b32_e32 v59, v107
	v_xor_b32_e32 v60, 0x80000000, v57
	v_mov_b32_e32 v61, v57
	v_pk_mul_f32 v[58:59], v[56:57], v[58:59] op_sel:[1,0] op_sel_hi:[0,1]
	v_pk_mul_f32 v[60:61], v[14:15], v[60:61] op_sel:[1,0] op_sel_hi:[0,1]
	v_pk_fma_f32 v[58:59], v[56:57], v[106:107], v[58:59] op_sel_hi:[1,0,1]
	v_pk_fma_f32 v[56:57], v[14:15], v[56:57], v[60:61] op_sel_hi:[1,0,1]
	v_xor_b32_e32 v60, 0x80000000, v85
	v_mov_b32_e32 v61, v85
	v_pk_mul_f32 v[60:61], v[56:57], v[60:61] op_sel:[1,0] op_sel_hi:[0,1]
	v_pk_fma_f32 v[60:61], v[56:57], v[84:85], v[60:61] op_sel_hi:[1,0,1]
	ds_write2_b64 v74, v[58:59], v[60:61] offset0:64 offset1:80
	v_xor_b32_e32 v58, 0x80000000, v57
	v_mov_b32_e32 v59, v57
	v_pk_mul_f32 v[58:59], v[14:15], v[58:59] op_sel:[1,0] op_sel_hi:[0,1]
	v_pk_fma_f32 v[56:57], v[14:15], v[56:57], v[58:59] op_sel_hi:[1,0,1]
	v_xor_b32_e32 v58, 0x80000000, v101
	v_mov_b32_e32 v59, v101
	v_xor_b32_e32 v60, 0x80000000, v57
	v_mov_b32_e32 v61, v57
	v_pk_mul_f32 v[58:59], v[56:57], v[58:59] op_sel:[1,0] op_sel_hi:[0,1]
	v_pk_mul_f32 v[60:61], v[14:15], v[60:61] op_sel:[1,0] op_sel_hi:[0,1]
	v_pk_fma_f32 v[58:59], v[56:57], v[100:101], v[58:59] op_sel_hi:[1,0,1]
	v_pk_fma_f32 v[56:57], v[14:15], v[56:57], v[60:61] op_sel_hi:[1,0,1]
	v_xor_b32_e32 v60, 0x80000000, v87
	v_mov_b32_e32 v61, v87
	v_pk_mul_f32 v[60:61], v[56:57], v[60:61] op_sel:[1,0] op_sel_hi:[0,1]
	v_pk_fma_f32 v[60:61], v[56:57], v[86:87], v[60:61] op_sel_hi:[1,0,1]
	ds_write2_b64 v73, v[58:59], v[60:61] offset0:96 offset1:112
	v_xor_b32_e32 v58, 0x80000000, v57
	v_mov_b32_e32 v59, v57
	v_pk_mul_f32 v[58:59], v[14:15], v[58:59] op_sel:[1,0] op_sel_hi:[0,1]
	v_pk_fma_f32 v[56:57], v[14:15], v[56:57], v[58:59] op_sel_hi:[1,0,1]
	v_xor_b32_e32 v58, 0x80000000, v47
	v_mov_b32_e32 v59, v47
	v_pk_mul_f32 v[58:59], v[56:57], v[58:59] op_sel:[1,0] op_sel_hi:[0,1]
	v_pk_fma_f32 v[46:47], v[56:57], v[46:47], v[58:59] op_sel_hi:[1,0,1]
	v_xor_b32_e32 v58, 0x80000000, v57
	v_mov_b32_e32 v59, v57
	v_pk_mul_f32 v[58:59], v[14:15], v[58:59] op_sel:[1,0] op_sel_hi:[0,1]
	v_pk_fma_f32 v[56:57], v[14:15], v[56:57], v[58:59] op_sel_hi:[1,0,1]
	v_xor_b32_e32 v58, 0x80000000, v93
	v_mov_b32_e32 v59, v93
	v_pk_mul_f32 v[58:59], v[56:57], v[58:59] op_sel:[1,0] op_sel_hi:[0,1]
	v_pk_fma_f32 v[58:59], v[56:57], v[92:93], v[58:59] op_sel_hi:[1,0,1]
	ds_write2_b64 v72, v[46:47], v[58:59] offset0:128 offset1:144
	v_xor_b32_e32 v46, 0x80000000, v57
	v_mov_b32_e32 v47, v57
	v_pk_mul_f32 v[46:47], v[14:15], v[46:47] op_sel:[1,0] op_sel_hi:[0,1]
	v_pk_fma_f32 v[46:47], v[14:15], v[56:57], v[46:47] op_sel_hi:[1,0,1]
	v_xor_b32_e32 v56, 0x80000000, v51
	v_mov_b32_e32 v57, v51
	v_pk_mul_f32 v[56:57], v[46:47], v[56:57] op_sel:[1,0] op_sel_hi:[0,1]
	v_pk_fma_f32 v[50:51], v[46:47], v[50:51], v[56:57] op_sel_hi:[1,0,1]
	v_xor_b32_e32 v56, 0x80000000, v47
	v_mov_b32_e32 v57, v47
	v_pk_mul_f32 v[56:57], v[14:15], v[56:57] op_sel:[1,0] op_sel_hi:[0,1]
	v_pk_fma_f32 v[46:47], v[14:15], v[46:47], v[56:57] op_sel_hi:[1,0,1]
	v_xor_b32_e32 v56, 0x80000000, v95
	v_mov_b32_e32 v57, v95
	v_pk_mul_f32 v[56:57], v[46:47], v[56:57] op_sel:[1,0] op_sel_hi:[0,1]
	v_pk_fma_f32 v[56:57], v[46:47], v[94:95], v[56:57] op_sel_hi:[1,0,1]
	ds_write2_b64 v71, v[50:51], v[56:57] offset0:160 offset1:176
	v_xor_b32_e32 v50, 0x80000000, v47
	v_mov_b32_e32 v51, v47
	v_pk_mul_f32 v[50:51], v[14:15], v[50:51] op_sel:[1,0] op_sel_hi:[0,1]
	v_pk_fma_f32 v[46:47], v[14:15], v[46:47], v[50:51] op_sel_hi:[1,0,1]
	v_xor_b32_e32 v50, 0x80000000, v39
	v_mov_b32_e32 v51, v39
	v_pk_mul_f32 v[50:51], v[50:51], v[46:47] op_sel:[0,1] op_sel_hi:[1,0]
	s_nop 0
	v_pk_fma_f32 v[38:39], v[38:39], v[46:47], v[50:51] op_sel_hi:[0,1,1]
	v_xor_b32_e32 v50, 0x80000000, v47
	v_mov_b32_e32 v51, v47
	v_pk_mul_f32 v[50:51], v[14:15], v[50:51] op_sel:[1,0] op_sel_hi:[0,1]
	v_pk_fma_f32 v[46:47], v[14:15], v[46:47], v[50:51] op_sel_hi:[1,0,1]
	v_xor_b32_e32 v50, 0x80000000, v79
	v_mov_b32_e32 v51, v79
	v_pk_mul_f32 v[50:51], v[46:47], v[50:51] op_sel:[1,0] op_sel_hi:[0,1]
	v_pk_fma_f32 v[50:51], v[46:47], v[78:79], v[50:51] op_sel_hi:[1,0,1]
	ds_write2_b64 v70, v[38:39], v[50:51] offset0:192 offset1:208
	v_xor_b32_e32 v38, 0x80000000, v47
	v_mov_b32_e32 v39, v47
	v_pk_mul_f32 v[38:39], v[14:15], v[38:39] op_sel:[1,0] op_sel_hi:[0,1]
	v_pk_fma_f32 v[38:39], v[14:15], v[46:47], v[38:39] op_sel_hi:[1,0,1]
	v_xor_b32_e32 v46, 0x80000000, v43
	v_mov_b32_e32 v47, v43
	v_pk_mul_f32 v[46:47], v[46:47], v[38:39] op_sel:[0,1] op_sel_hi:[1,0]
	s_nop 0
	v_pk_fma_f32 v[42:43], v[42:43], v[38:39], v[46:47] op_sel_hi:[0,1,1]
	v_xor_b32_e32 v46, 0x80000000, v39
	v_mov_b32_e32 v47, v39
	v_pk_mul_f32 v[46:47], v[14:15], v[46:47] op_sel:[1,0] op_sel_hi:[0,1]
	v_pk_fma_f32 v[38:39], v[14:15], v[38:39], v[46:47] op_sel_hi:[1,0,1]
	v_xor_b32_e32 v46, 0x80000000, v83
	v_mov_b32_e32 v47, v83
	v_pk_mul_f32 v[46:47], v[38:39], v[46:47] op_sel:[1,0] op_sel_hi:[0,1]
	v_pk_fma_f32 v[46:47], v[38:39], v[82:83], v[46:47] op_sel_hi:[1,0,1]
	ds_write2_b64 v69, v[42:43], v[46:47] offset0:224 offset1:240
	v_xor_b32_e32 v42, 0x80000000, v39
	v_mov_b32_e32 v43, v39
	v_pk_mul_f32 v[42:43], v[14:15], v[42:43] op_sel:[1,0] op_sel_hi:[0,1]
	v_pk_fma_f32 v[38:39], v[14:15], v[38:39], v[42:43] op_sel_hi:[1,0,1]
	v_xor_b32_e32 v42, 0x80000000, v31
	v_mov_b32_e32 v43, v31
	v_pk_mul_f32 v[42:43], v[42:43], v[38:39] op_sel:[0,1] op_sel_hi:[1,0]
	s_nop 0
	v_pk_fma_f32 v[30:31], v[30:31], v[38:39], v[42:43] op_sel_hi:[0,1,1]
	v_xor_b32_e32 v42, 0x80000000, v39
	v_mov_b32_e32 v43, v39
	v_pk_mul_f32 v[42:43], v[14:15], v[42:43] op_sel:[1,0] op_sel_hi:[0,1]
	v_pk_fma_f32 v[38:39], v[14:15], v[38:39], v[42:43] op_sel_hi:[1,0,1]
	v_xor_b32_e32 v42, 0x80000000, v81
	v_mov_b32_e32 v43, v81
	v_pk_mul_f32 v[42:43], v[42:43], v[38:39] op_sel:[0,1] op_sel_hi:[1,0]
	s_nop 0
	v_pk_fma_f32 v[42:43], v[80:81], v[38:39], v[42:43] op_sel_hi:[0,1,1]
	ds_write2_b64 v68, v[30:31], v[42:43] offset1:16
	v_xor_b32_e32 v30, 0x80000000, v39
	v_mov_b32_e32 v31, v39
	v_pk_mul_f32 v[30:31], v[14:15], v[30:31] op_sel:[1,0] op_sel_hi:[0,1]
	v_pk_fma_f32 v[30:31], v[14:15], v[38:39], v[30:31] op_sel_hi:[1,0,1]
	v_xor_b32_e32 v38, 0x80000000, v35
	v_mov_b32_e32 v39, v35
	v_pk_mul_f32 v[38:39], v[38:39], v[30:31] op_sel:[0,1] op_sel_hi:[1,0]
	s_nop 0
	v_pk_fma_f32 v[34:35], v[34:35], v[30:31], v[38:39] op_sel_hi:[0,1,1]
	v_xor_b32_e32 v38, 0x80000000, v31
	v_mov_b32_e32 v39, v31
	v_pk_mul_f32 v[38:39], v[14:15], v[38:39] op_sel:[1,0] op_sel_hi:[0,1]
	v_pk_fma_f32 v[30:31], v[14:15], v[30:31], v[38:39] op_sel_hi:[1,0,1]
	v_xor_b32_e32 v38, 0x80000000, v55
	v_mov_b32_e32 v39, v55
	v_pk_mul_f32 v[38:39], v[38:39], v[30:31] op_sel:[0,1] op_sel_hi:[1,0]
	s_nop 0
	v_pk_fma_f32 v[38:39], v[54:55], v[30:31], v[38:39] op_sel_hi:[0,1,1]
	ds_write2_b64 v67, v[34:35], v[38:39] offset0:32 offset1:48
	v_xor_b32_e32 v34, 0x80000000, v31
	v_mov_b32_e32 v35, v31
	v_pk_mul_f32 v[34:35], v[14:15], v[34:35] op_sel:[1,0] op_sel_hi:[0,1]
	v_pk_fma_f32 v[30:31], v[14:15], v[30:31], v[34:35] op_sel_hi:[1,0,1]
	v_xor_b32_e32 v34, 0x80000000, v27
	v_mov_b32_e32 v35, v27
	v_pk_mul_f32 v[34:35], v[34:35], v[30:31] op_sel:[0,1] op_sel_hi:[1,0]
	s_nop 0
	v_pk_fma_f32 v[26:27], v[26:27], v[30:31], v[34:35] op_sel_hi:[0,1,1]
	v_xor_b32_e32 v34, 0x80000000, v31
	v_mov_b32_e32 v35, v31
	v_pk_mul_f32 v[34:35], v[14:15], v[34:35] op_sel:[1,0] op_sel_hi:[0,1]
	v_pk_fma_f32 v[30:31], v[14:15], v[30:31], v[34:35] op_sel_hi:[1,0,1]
	v_xor_b32_e32 v34, 0x80000000, v49
	v_mov_b32_e32 v35, v49
	v_pk_mul_f32 v[34:35], v[34:35], v[30:31] op_sel:[0,1] op_sel_hi:[1,0]
	s_nop 0
	v_pk_fma_f32 v[34:35], v[48:49], v[30:31], v[34:35] op_sel_hi:[0,1,1]
	ds_write2_b64 v66, v[26:27], v[34:35] offset0:64 offset1:80
	v_xor_b32_e32 v26, 0x80000000, v31
	v_mov_b32_e32 v27, v31
	v_pk_mul_f32 v[26:27], v[14:15], v[26:27] op_sel:[1,0] op_sel_hi:[0,1]
	v_pk_fma_f32 v[26:27], v[14:15], v[30:31], v[26:27] op_sel_hi:[1,0,1]
	v_xor_b32_e32 v30, 0x80000000, v29
	v_mov_b32_e32 v31, v29
	v_pk_mul_f32 v[30:31], v[30:31], v[26:27] op_sel:[0,1] op_sel_hi:[1,0]
	s_nop 0
	v_pk_fma_f32 v[28:29], v[28:29], v[26:27], v[30:31] op_sel_hi:[0,1,1]
	v_xor_b32_e32 v30, 0x80000000, v27
	v_mov_b32_e32 v31, v27
	v_pk_mul_f32 v[30:31], v[14:15], v[30:31] op_sel:[1,0] op_sel_hi:[0,1]
	v_pk_fma_f32 v[26:27], v[14:15], v[26:27], v[30:31] op_sel_hi:[1,0,1]
	v_xor_b32_e32 v30, 0x80000000, v53
	v_mov_b32_e32 v31, v53
	v_pk_mul_f32 v[30:31], v[30:31], v[26:27] op_sel:[0,1] op_sel_hi:[1,0]
	s_nop 0
	v_pk_fma_f32 v[30:31], v[52:53], v[26:27], v[30:31] op_sel_hi:[0,1,1]
	ds_write2_b64 v65, v[28:29], v[30:31] offset0:96 offset1:112
	v_xor_b32_e32 v28, 0x80000000, v27
	v_mov_b32_e32 v29, v27
	v_pk_mul_f32 v[28:29], v[14:15], v[28:29] op_sel:[1,0] op_sel_hi:[0,1]
	v_pk_fma_f32 v[26:27], v[14:15], v[26:27], v[28:29] op_sel_hi:[1,0,1]
	v_xor_b32_e32 v28, 0x80000000, v23
	v_mov_b32_e32 v29, v23
	v_pk_mul_f32 v[28:29], v[28:29], v[26:27] op_sel:[0,1] op_sel_hi:[1,0]
	s_nop 0
	v_pk_fma_f32 v[22:23], v[22:23], v[26:27], v[28:29] op_sel_hi:[0,1,1]
	v_xor_b32_e32 v28, 0x80000000, v27
	v_mov_b32_e32 v29, v27
	v_pk_mul_f32 v[28:29], v[14:15], v[28:29] op_sel:[1,0] op_sel_hi:[0,1]
	v_pk_fma_f32 v[26:27], v[14:15], v[26:27], v[28:29] op_sel_hi:[1,0,1]
	v_xor_b32_e32 v28, 0x80000000, v41
	v_mov_b32_e32 v29, v41
	v_pk_mul_f32 v[28:29], v[28:29], v[26:27] op_sel:[0,1] op_sel_hi:[1,0]
	s_nop 0
	v_pk_fma_f32 v[28:29], v[40:41], v[26:27], v[28:29] op_sel_hi:[0,1,1]
	ds_write2_b64 v64, v[22:23], v[28:29] offset0:128 offset1:144
	v_xor_b32_e32 v22, 0x80000000, v27
	v_mov_b32_e32 v23, v27
	v_pk_mul_f32 v[22:23], v[14:15], v[22:23] op_sel:[1,0] op_sel_hi:[0,1]
	v_pk_fma_f32 v[22:23], v[14:15], v[26:27], v[22:23] op_sel_hi:[1,0,1]
	v_xor_b32_e32 v26, 0x80000000, v25
	v_mov_b32_e32 v27, v25
	v_pk_mul_f32 v[26:27], v[26:27], v[22:23] op_sel:[0,1] op_sel_hi:[1,0]
	s_nop 0
	v_pk_fma_f32 v[24:25], v[24:25], v[22:23], v[26:27] op_sel_hi:[0,1,1]
	v_xor_b32_e32 v26, 0x80000000, v23
	v_mov_b32_e32 v27, v23
	v_pk_mul_f32 v[26:27], v[14:15], v[26:27] op_sel:[1,0] op_sel_hi:[0,1]
	v_pk_fma_f32 v[22:23], v[14:15], v[22:23], v[26:27] op_sel_hi:[1,0,1]
	v_xor_b32_e32 v26, 0x80000000, v45
	v_mov_b32_e32 v27, v45
	v_pk_mul_f32 v[26:27], v[26:27], v[22:23] op_sel:[0,1] op_sel_hi:[1,0]
	s_nop 0
	v_pk_fma_f32 v[26:27], v[44:45], v[22:23], v[26:27] op_sel_hi:[0,1,1]
	ds_write2_b64 v63, v[24:25], v[26:27] offset0:160 offset1:176
	v_xor_b32_e32 v24, 0x80000000, v23
	v_mov_b32_e32 v25, v23
	v_pk_mul_f32 v[24:25], v[14:15], v[24:25] op_sel:[1,0] op_sel_hi:[0,1]
	v_pk_fma_f32 v[22:23], v[14:15], v[22:23], v[24:25] op_sel_hi:[1,0,1]
	v_xor_b32_e32 v24, 0x80000000, v19
	v_mov_b32_e32 v25, v19
	v_pk_mul_f32 v[24:25], v[24:25], v[22:23] op_sel:[0,1] op_sel_hi:[1,0]
	s_nop 0
	v_pk_fma_f32 v[18:19], v[18:19], v[22:23], v[24:25] op_sel_hi:[0,1,1]
	v_xor_b32_e32 v24, 0x80000000, v23
	v_mov_b32_e32 v25, v23
	v_pk_mul_f32 v[24:25], v[14:15], v[24:25] op_sel:[1,0] op_sel_hi:[0,1]
	v_pk_fma_f32 v[22:23], v[14:15], v[22:23], v[24:25] op_sel_hi:[1,0,1]
	v_xor_b32_e32 v24, 0x80000000, v33
	v_mov_b32_e32 v25, v33
	v_pk_mul_f32 v[24:25], v[24:25], v[22:23] op_sel:[0,1] op_sel_hi:[1,0]
	s_nop 0
	v_pk_fma_f32 v[24:25], v[32:33], v[22:23], v[24:25] op_sel_hi:[0,1,1]
	ds_write2_b64 v62, v[18:19], v[24:25] offset0:192 offset1:208
	v_xor_b32_e32 v18, 0x80000000, v23
	v_mov_b32_e32 v19, v23
	v_pk_mul_f32 v[18:19], v[14:15], v[18:19] op_sel:[1,0] op_sel_hi:[0,1]
	v_pk_fma_f32 v[18:19], v[14:15], v[22:23], v[18:19] op_sel_hi:[1,0,1]
	v_xor_b32_e32 v22, 0x80000000, v21
	v_mov_b32_e32 v23, v21
	v_pk_mul_f32 v[22:23], v[22:23], v[18:19] op_sel:[0,1] op_sel_hi:[1,0]
	s_nop 0
	v_pk_fma_f32 v[20:21], v[20:21], v[18:19], v[22:23] op_sel_hi:[0,1,1]
	v_xor_b32_e32 v22, 0x80000000, v19
	v_mov_b32_e32 v23, v19
	v_pk_mul_f32 v[22:23], v[14:15], v[22:23] op_sel:[1,0] op_sel_hi:[0,1]
	v_pk_fma_f32 v[14:15], v[14:15], v[18:19], v[22:23] op_sel_hi:[1,0,1]
	v_xor_b32_e32 v18, 0x80000000, v37
	v_mov_b32_e32 v19, v37
	v_pk_mul_f32 v[18:19], v[18:19], v[14:15] op_sel:[0,1] op_sel_hi:[1,0]
	s_nop 0
	v_pk_fma_f32 v[14:15], v[36:37], v[14:15], v[18:19] op_sel_hi:[0,1,1]
	ds_write2_b64 v13, v[20:21], v[14:15] offset0:224 offset1:240
	v_mov_b32_e32 v14, v1
	v_mov_b32_e32 v10, v178
	v_mov_b32_e32 v13, v177
	s_waitcnt lgkmcnt(0)
	s_barrier
	v_mov_b32_e32 v50, v168
	v_xor_b32_e32 v18, 1, v13
	v_lshlrev_b32_e32 v10, 3, v10
	v_lshlrev_b32_e32 v18, 3, v18
	v_add3_u32 v20, 0, v18, v10
	v_xor_b32_e32 v18, 2, v13
	v_lshlrev_b32_e32 v18, 3, v18
	v_xor_b32_e32 v26, 5, v13
	v_add3_u32 v22, 0, v18, v10
	v_xor_b32_e32 v18, 3, v13
	v_lshlrev_b32_e32 v26, 3, v26
	v_lshlrev_b32_e32 v15, 3, v13
	v_lshlrev_b32_e32 v18, 3, v18
	v_add3_u32 v28, 0, v26, v10
	v_xor_b32_e32 v26, 6, v13
	v_add3_u32 v15, 0, v15, v10
	v_add3_u32 v24, 0, v18, v10
	v_lshlrev_b32_e32 v26, 3, v26
	v_xor_b32_e32 v34, 9, v13
	ds_read_b64 v[18:19], v15
	ds_read_b64 v[20:21], v20
	ds_read_b64 v[22:23], v22
	ds_read_b64 v[24:25], v24
	v_xor_b32_e32 v15, 4, v13
	v_add3_u32 v30, 0, v26, v10
	v_xor_b32_e32 v26, 7, v13
	v_lshlrev_b32_e32 v34, 3, v34
	v_lshlrev_b32_e32 v15, 3, v15
	v_lshlrev_b32_e32 v26, 3, v26
	v_add3_u32 v36, 0, v34, v10
	v_xor_b32_e32 v34, 10, v13
	v_add3_u32 v15, 0, v15, v10
	v_add3_u32 v32, 0, v26, v10
	v_lshlrev_b32_e32 v34, 3, v34
	ds_read_b64 v[26:27], v15
	ds_read_b64 v[28:29], v28
	ds_read_b64 v[30:31], v30
	ds_read_b64 v[32:33], v32
	v_xor_b32_e32 v15, 8, v13
	v_add3_u32 v38, 0, v34, v10
	v_xor_b32_e32 v34, 11, v13
	v_lshlrev_b32_e32 v15, 3, v15
	v_lshlrev_b32_e32 v34, 3, v34
	v_xor_b32_e32 v42, 13, v13
	v_add3_u32 v15, 0, v15, v10
	v_add3_u32 v40, 0, v34, v10
	v_lshlrev_b32_e32 v42, 3, v42
	ds_read_b64 v[34:35], v15
	ds_read_b64 v[36:37], v36
	ds_read_b64 v[38:39], v38
	ds_read_b64 v[40:41], v40
	v_xor_b32_e32 v15, 12, v13
	v_add3_u32 v44, 0, v42, v10
	v_xor_b32_e32 v42, 14, v13
	v_xor_b32_e32 v13, 15, v13
	v_lshlrev_b32_e32 v15, 3, v15
	v_lshlrev_b32_e32 v42, 3, v42
	v_lshlrev_b32_e32 v13, 3, v13
	v_add3_u32 v15, 0, v15, v10
	v_add3_u32 v46, 0, v42, v10
	v_add3_u32 v10, 0, v13, v10
	ds_read_b64 v[42:43], v15
	ds_read_b64 v[44:45], v44
	ds_read_b64 v[46:47], v46
	ds_read_b64 v[48:49], v10
	v_mov_b32_e32 v10, v164
	v_mov_b32_e32 v13, v167
	v_mov_b32_e32 v10, v165
	s_waitcnt lgkmcnt(7)
	v_pk_add_f32 v[54:55], v[18:19], v[34:35]
	v_mov_b32_e32 v10, v166
	v_pk_add_f32 v[18:19], v[18:19], v[34:35] neg_lo:[0,1] neg_hi:[0,1]
	s_waitcnt lgkmcnt(6)
	v_pk_add_f32 v[34:35], v[20:21], v[36:37]
	v_pk_add_f32 v[20:21], v[20:21], v[36:37] neg_lo:[0,1] neg_hi:[0,1]
	v_mov_b32_e32 v13, v169
	v_mov_b32_e32 v52, v170
	v_xor_b32_e32 v36, 0x80000000, v21
	v_mov_b32_e32 v37, v20
	v_ashrrev_i32_e32 v15, 31, v14
	v_pk_mul_f32 v[36:37], v[36:37], v[52:53] op_sel_hi:[1,0] neg_lo:[0,1] neg_hi:[0,1]
	v_mov_b32_e32 v13, v171
	v_pk_fma_f32 v[20:21], v[20:21], v[10:11], v[36:37] op_sel_hi:[1,0,1]
	s_waitcnt lgkmcnt(5)
	v_pk_add_f32 v[36:37], v[22:23], v[38:39]
	v_pk_add_f32 v[22:23], v[22:23], v[38:39] neg_lo:[0,1] neg_hi:[0,1]
	s_movk_i32 s85, 0x1000
	v_xor_b32_e32 v38, 0x80000000, v23
	v_mov_b32_e32 v39, v22
	v_pk_mul_f32 v[38:39], v[38:39], v[50:51] op_sel_hi:[1,0] neg_lo:[0,1] neg_hi:[0,1]
	v_mov_b32_e32 v13, v172
	v_pk_fma_f32 v[22:23], v[22:23], v[50:51], v[38:39] op_sel_hi:[1,0,1]
	s_waitcnt lgkmcnt(4)
	v_pk_add_f32 v[38:39], v[24:25], v[40:41]
	v_pk_add_f32 v[24:25], v[24:25], v[40:41] neg_lo:[0,1] neg_hi:[0,1]
	s_movk_i32 s84, 0x2000
	v_pk_mul_f32 v[40:41], v[24:25], v[52:53] op_sel_hi:[1,0]
	v_xor_b32_e32 v56, 0x80000000, v25
	v_mov_b32_e32 v57, v24
	v_pk_fma_f32 v[24:25], v[56:57], v[10:11], v[40:41] op_sel_hi:[1,0,1] neg_lo:[0,1,0] neg_hi:[0,1,0]
	s_waitcnt lgkmcnt(3)
	v_pk_add_f32 v[40:41], v[26:27], v[42:43]
	v_pk_add_f32 v[26:27], v[26:27], v[42:43] neg_lo:[0,1] neg_hi:[0,1]
	v_mov_b32_e32 v13, v177
	v_xor_b32_e32 v43, 0x80000000, v26
	v_mov_b32_e32 v42, v27
	s_waitcnt lgkmcnt(2)
	v_pk_add_f32 v[26:27], v[28:29], v[44:45]
	v_pk_add_f32 v[28:29], v[28:29], v[44:45] neg_lo:[0,1] neg_hi:[0,1]
	s_movk_i32 s88, 0x6000
	v_pk_mul_f32 v[44:45], v[28:29], v[52:53] op_sel_hi:[1,0] neg_lo:[0,1] neg_hi:[0,1]
	v_xor_b32_e32 v56, 0x80000000, v29
	v_mov_b32_e32 v57, v28
	v_pk_fma_f32 v[28:29], v[56:57], v[10:11], v[44:45] op_sel_hi:[1,0,1] neg_lo:[0,1,0] neg_hi:[0,1,0]
	s_waitcnt lgkmcnt(1)
	v_pk_add_f32 v[44:45], v[30:31], v[46:47]
	v_pk_add_f32 v[30:31], v[30:31], v[46:47] neg_lo:[0,1] neg_hi:[0,1]
	s_mov_b32 s0, 0x8000
	v_xor_b32_e32 v46, 0x80000000, v31
	v_mov_b32_e32 v47, v30
	v_pk_mul_f32 v[46:47], v[46:47], v[50:51] op_sel_hi:[1,0] neg_lo:[0,1] neg_hi:[0,1]
	s_movk_i32 s86, 0x5000
	v_pk_fma_f32 v[30:31], v[30:31], v[50:51], v[46:47] op_sel_hi:[1,0,1] neg_lo:[0,1,0] neg_hi:[0,1,0]
	s_waitcnt lgkmcnt(0)
	v_pk_add_f32 v[46:47], v[32:33], v[48:49]
	v_pk_add_f32 v[32:33], v[32:33], v[48:49] neg_lo:[0,1] neg_hi:[0,1]
	v_mov_b32_e32 v72, v165
	v_xor_b32_e32 v48, 0x80000000, v33
	v_mov_b32_e32 v49, v32
	v_pk_mul_f32 v[48:49], v[48:49], v[52:53] op_sel_hi:[1,0] neg_lo:[0,1] neg_hi:[0,1]
	v_pk_add_f32 v[52:53], v[34:35], v[26:27]
	v_pk_add_f32 v[26:27], v[34:35], v[26:27] neg_lo:[0,1] neg_hi:[0,1]
	v_pk_fma_f32 v[32:33], v[32:33], v[10:11], v[48:49] op_sel_hi:[1,0,1] neg_lo:[0,1,0] neg_hi:[0,1,0]
	v_xor_b32_e32 v34, 0x80000000, v27
	v_mov_b32_e32 v35, v26
	v_pk_mul_f32 v[34:35], v[34:35], v[50:51] op_sel_hi:[1,0] neg_lo:[0,1] neg_hi:[0,1]
	v_pk_add_f32 v[48:49], v[54:55], v[40:41]
	v_pk_fma_f32 v[26:27], v[26:27], v[50:51], v[34:35] op_sel_hi:[1,0,1]
	v_pk_add_f32 v[34:35], v[36:37], v[44:45]
	v_pk_add_f32 v[36:37], v[36:37], v[44:45] neg_lo:[0,1] neg_hi:[0,1]
	v_pk_add_f32 v[40:41], v[54:55], v[40:41] neg_lo:[0,1] neg_hi:[0,1]
	v_xor_b32_e32 v45, 0x80000000, v36
	v_mov_b32_e32 v44, v37
	v_pk_add_f32 v[36:37], v[38:39], v[46:47]
	v_pk_add_f32 v[38:39], v[38:39], v[46:47] neg_lo:[0,1] neg_hi:[0,1]
	v_mov_b32_e32 v10, v179
	v_xor_b32_e32 v46, 0x80000000, v39
	v_mov_b32_e32 v47, v38
	v_pk_mul_f32 v[46:47], v[46:47], v[50:51] op_sel_hi:[1,0] neg_lo:[0,1] neg_hi:[0,1]
	v_mov_b32_e32 v74, v167
	v_pk_fma_f32 v[38:39], v[38:39], v[50:51], v[46:47] op_sel_hi:[1,0,1] neg_lo:[0,1,0] neg_hi:[0,1,0]
	v_pk_add_f32 v[46:47], v[48:49], v[34:35]
	v_pk_add_f32 v[34:35], v[48:49], v[34:35] neg_lo:[0,1] neg_hi:[0,1]
	v_pk_add_f32 v[48:49], v[52:53], v[36:37]
	v_pk_add_f32 v[36:37], v[52:53], v[36:37] neg_lo:[0,1] neg_hi:[0,1]
	v_mov_b32_e32 v76, v169
	v_xor_b32_e32 v53, 0x80000000, v36
	v_mov_b32_e32 v52, v37
	v_pk_add_f32 v[36:37], v[46:47], v[48:49]
	v_pk_add_f32 v[46:47], v[46:47], v[48:49] neg_lo:[0,1] neg_hi:[0,1]
	v_pk_add_f32 v[48:49], v[34:35], v[52:53]
	v_pk_add_f32 v[34:35], v[34:35], v[52:53] neg_lo:[0,1] neg_hi:[0,1]
	v_pk_add_f32 v[52:53], v[40:41], v[44:45]
	v_pk_add_f32 v[40:41], v[40:41], v[44:45] neg_lo:[0,1] neg_hi:[0,1]
	v_pk_add_f32 v[44:45], v[26:27], v[38:39]
	v_pk_add_f32 v[26:27], v[26:27], v[38:39] neg_lo:[0,1] neg_hi:[0,1]
	v_mov_b32_e32 v78, v171
	v_xor_b32_e32 v39, 0x80000000, v26
	v_mov_b32_e32 v38, v27
	v_pk_add_f32 v[26:27], v[52:53], v[44:45]
	v_pk_add_f32 v[44:45], v[52:53], v[44:45] neg_lo:[0,1] neg_hi:[0,1]
	v_pk_add_f32 v[52:53], v[40:41], v[38:39]
	v_pk_add_f32 v[38:39], v[40:41], v[38:39] neg_lo:[0,1] neg_hi:[0,1]
	v_pk_add_f32 v[40:41], v[18:19], v[42:43]
	v_pk_add_f32 v[18:19], v[18:19], v[42:43] neg_lo:[0,1] neg_hi:[0,1]
	v_pk_add_f32 v[42:43], v[20:21], v[28:29]
	v_pk_add_f32 v[20:21], v[20:21], v[28:29] neg_lo:[0,1] neg_hi:[0,1]
	v_mov_b32_e32 v83, v11
	v_xor_b32_e32 v28, 0x80000000, v21
	v_mov_b32_e32 v29, v20
	v_pk_mul_f32 v[28:29], v[50:51], v[28:29] op_sel_hi:[0,1] neg_lo:[1,0] neg_hi:[1,0]
	v_pk_fma_f32 v[20:21], v[50:51], v[20:21], v[28:29] op_sel_hi:[0,1,1]
	v_pk_add_f32 v[28:29], v[22:23], v[30:31]
	v_pk_add_f32 v[22:23], v[22:23], v[30:31] neg_lo:[0,1] neg_hi:[0,1]
	s_mov_b32 s1, 0xe000
	v_xor_b32_e32 v31, 0x80000000, v22
	v_mov_b32_e32 v30, v23
	v_pk_add_f32 v[22:23], v[24:25], v[32:33]
	v_pk_add_f32 v[24:25], v[24:25], v[32:33] neg_lo:[0,1] neg_hi:[0,1]
	s_mov_b32 s8, 0x8000
	v_xor_b32_e32 v32, 0x80000000, v25
	v_mov_b32_e32 v33, v24
	v_pk_mul_f32 v[32:33], v[50:51], v[32:33] op_sel_hi:[0,1] neg_lo:[1,0] neg_hi:[1,0]
	v_pk_fma_f32 v[24:25], v[50:51], v[24:25], v[32:33] op_sel_hi:[0,1,1] neg_lo:[1,0,0] neg_hi:[1,0,0]
	v_pk_add_f32 v[32:33], v[40:41], v[28:29]
	v_pk_add_f32 v[28:29], v[40:41], v[28:29] neg_lo:[0,1] neg_hi:[0,1]
	v_pk_add_f32 v[40:41], v[42:43], v[22:23]
	v_pk_add_f32 v[22:23], v[42:43], v[22:23] neg_lo:[0,1] neg_hi:[0,1]
	v_mov_b32_e32 v50, v168
	v_xor_b32_e32 v43, 0x80000000, v22
	v_mov_b32_e32 v42, v23
	v_pk_add_f32 v[22:23], v[32:33], v[40:41]
	v_pk_add_f32 v[32:33], v[32:33], v[40:41] neg_lo:[0,1] neg_hi:[0,1]
	v_pk_add_f32 v[40:41], v[28:29], v[42:43]
	v_pk_add_f32 v[28:29], v[28:29], v[42:43] neg_lo:[0,1] neg_hi:[0,1]
	v_pk_add_f32 v[42:43], v[18:19], v[30:31]
	v_pk_add_f32 v[18:19], v[18:19], v[30:31] neg_lo:[0,1] neg_hi:[0,1]
	v_pk_add_f32 v[30:31], v[20:21], v[24:25]
	v_pk_add_f32 v[20:21], v[20:21], v[24:25] neg_lo:[0,1] neg_hi:[0,1]
	s_mov_b32 s7, 0xa000
	v_xor_b32_e32 v25, 0x80000000, v20
	v_mov_b32_e32 v24, v21
	v_pk_add_f32 v[20:21], v[42:43], v[30:31]
	v_pk_add_f32 v[30:31], v[42:43], v[30:31] neg_lo:[0,1] neg_hi:[0,1]
	v_pk_add_f32 v[42:43], v[18:19], v[24:25]
	v_pk_add_f32 v[18:19], v[18:19], v[24:25] neg_lo:[0,1] neg_hi:[0,1]
	v_lshl_add_u64 v[24:25], v[14:15], 3, s[48:49]
	global_store_dwordx2 v[24:25], v[36:37], off
	v_add_u32_e32 v24, 0x200, v14
	v_ashrrev_i32_e32 v25, 31, v24
	v_lshl_add_u64 v[24:25], v[24:25], 3, s[48:49]
	global_store_dwordx2 v[24:25], v[22:23], off
	v_add_u32_e32 v22, 0x400, v14
	v_ashrrev_i32_e32 v23, 31, v22
	v_lshl_add_u64 v[22:23], v[22:23], 3, s[48:49]
	global_store_dwordx2 v[22:23], v[26:27], off
	v_add_u32_e32 v22, 0x600, v14
	v_ashrrev_i32_e32 v23, 31, v22
	v_lshl_add_u64 v[22:23], v[22:23], 3, s[48:49]
	global_store_dwordx2 v[22:23], v[20:21], off
	v_add_u32_e32 v20, 0x800, v14
	v_ashrrev_i32_e32 v21, 31, v20
	v_lshl_add_u64 v[20:21], v[20:21], 3, s[48:49]
	global_store_dwordx2 v[20:21], v[48:49], off
	v_add_u32_e32 v20, 0xa00, v14
	v_ashrrev_i32_e32 v21, 31, v20
	v_lshl_add_u64 v[20:21], v[20:21], 3, s[48:49]
	global_store_dwordx2 v[20:21], v[40:41], off
	v_add_u32_e32 v20, 0xc00, v14
	v_ashrrev_i32_e32 v21, 31, v20
	v_lshl_add_u64 v[20:21], v[20:21], 3, s[48:49]
	global_store_dwordx2 v[20:21], v[52:53], off
	v_add_u32_e32 v20, 0xe00, v14
	v_ashrrev_i32_e32 v21, 31, v20
	v_lshl_add_u64 v[20:21], v[20:21], 3, s[48:49]
	global_store_dwordx2 v[20:21], v[42:43], off
	v_add_u32_e32 v20, 0x1000, v14
	v_ashrrev_i32_e32 v21, 31, v20
	v_lshl_add_u64 v[20:21], v[20:21], 3, s[48:49]
	global_store_dwordx2 v[20:21], v[46:47], off
	v_add_u32_e32 v20, 0x1200, v14
	v_ashrrev_i32_e32 v21, 31, v20
	v_lshl_add_u64 v[20:21], v[20:21], 3, s[48:49]
	global_store_dwordx2 v[20:21], v[32:33], off
	v_add_u32_e32 v20, 0x1400, v14
	v_ashrrev_i32_e32 v21, 31, v20
	v_lshl_add_u64 v[20:21], v[20:21], 3, s[48:49]
	global_store_dwordx2 v[20:21], v[44:45], off
	v_add_u32_e32 v20, 0x1600, v14
	v_ashrrev_i32_e32 v21, 31, v20
	v_lshl_add_u64 v[20:21], v[20:21], 3, s[48:49]
	global_store_dwordx2 v[20:21], v[30:31], off
	v_add_u32_e32 v20, 0x1800, v14
	v_ashrrev_i32_e32 v21, 31, v20
	v_lshl_add_u64 v[20:21], v[20:21], 3, s[48:49]
	global_store_dwordx2 v[20:21], v[34:35], off
	v_add_u32_e32 v20, 0x1a00, v14
	v_ashrrev_i32_e32 v21, 31, v20
	v_lshl_add_u64 v[20:21], v[20:21], 3, s[48:49]
	global_store_dwordx2 v[20:21], v[28:29], off
	v_add_u32_e32 v20, 0x1c00, v14
	v_ashrrev_i32_e32 v21, 31, v20
	v_lshl_add_u64 v[20:21], v[20:21], 3, s[48:49]
	global_store_dwordx2 v[20:21], v[38:39], off
	v_add_u32_e32 v20, 0x1e00, v14
	v_ashrrev_i32_e32 v21, 31, v20
	v_lshl_add_u64 v[20:21], v[20:21], 3, s[48:49]
	global_store_dwordx2 v[20:21], v[18:19], off
	v_mov_b32_e32 v52, v170
	v_xor_b32_e32 v18, 1, v13
	v_lshlrev_b32_e32 v10, 3, v10
	v_lshlrev_b32_e32 v18, 3, v18
	v_add3_u32 v20, 0, v18, v10
	v_xor_b32_e32 v18, 2, v13
	v_lshlrev_b32_e32 v18, 3, v18
	v_xor_b32_e32 v26, 5, v13
	v_add3_u32 v22, 0, v18, v10
	v_xor_b32_e32 v18, 3, v13
	v_lshlrev_b32_e32 v26, 3, v26
	v_lshlrev_b32_e32 v15, 3, v13
	v_lshlrev_b32_e32 v18, 3, v18
	v_add3_u32 v28, 0, v26, v10
	v_xor_b32_e32 v26, 6, v13
	v_add3_u32 v15, 0, v15, v10
	v_add3_u32 v24, 0, v18, v10
	v_lshlrev_b32_e32 v26, 3, v26
	v_xor_b32_e32 v34, 9, v13
	ds_read_b64 v[18:19], v15
	ds_read_b64 v[20:21], v20
	ds_read_b64 v[22:23], v22
	ds_read_b64 v[24:25], v24
	v_xor_b32_e32 v15, 4, v13
	v_add3_u32 v30, 0, v26, v10
	v_xor_b32_e32 v26, 7, v13
	v_lshlrev_b32_e32 v34, 3, v34
	v_lshlrev_b32_e32 v15, 3, v15
	v_lshlrev_b32_e32 v26, 3, v26
	v_add3_u32 v36, 0, v34, v10
	v_xor_b32_e32 v34, 10, v13
	v_add3_u32 v15, 0, v15, v10
	v_add3_u32 v32, 0, v26, v10
	v_lshlrev_b32_e32 v34, 3, v34
	ds_read_b64 v[26:27], v15
	ds_read_b64 v[28:29], v28
	ds_read_b64 v[30:31], v30
	ds_read_b64 v[32:33], v32
	v_xor_b32_e32 v15, 8, v13
	v_add3_u32 v38, 0, v34, v10
	v_xor_b32_e32 v34, 11, v13
	v_lshlrev_b32_e32 v15, 3, v15
	v_lshlrev_b32_e32 v34, 3, v34
	v_xor_b32_e32 v42, 13, v13
	v_add3_u32 v15, 0, v15, v10
	v_add3_u32 v40, 0, v34, v10
	v_lshlrev_b32_e32 v42, 3, v42
	ds_read_b64 v[34:35], v15
	ds_read_b64 v[36:37], v36
	ds_read_b64 v[38:39], v38
	ds_read_b64 v[40:41], v40
	v_xor_b32_e32 v15, 12, v13
	v_add3_u32 v44, 0, v42, v10
	v_xor_b32_e32 v42, 14, v13
	v_xor_b32_e32 v13, 15, v13
	v_lshlrev_b32_e32 v15, 3, v15
	v_lshlrev_b32_e32 v42, 3, v42
	v_lshlrev_b32_e32 v13, 3, v13
	v_add3_u32 v15, 0, v15, v10
	v_add3_u32 v46, 0, v42, v10
	v_add3_u32 v10, 0, v13, v10
	ds_read_b64 v[42:43], v15
	ds_read_b64 v[44:45], v44
	ds_read_b64 v[46:47], v46
	ds_read_b64 v[48:49], v10
	v_mov_b32_e32 v10, v164
	v_mov_b32_e32 v13, v167
	v_mov_b32_e32 v10, v165
	s_waitcnt lgkmcnt(7)
	v_pk_add_f32 v[54:55], v[18:19], v[34:35]
	v_mov_b32_e32 v10, v166
	v_pk_add_f32 v[18:19], v[18:19], v[34:35] neg_lo:[0,1] neg_hi:[0,1]
	s_waitcnt lgkmcnt(6)
	v_pk_add_f32 v[34:35], v[20:21], v[36:37]
	v_pk_add_f32 v[20:21], v[20:21], v[36:37] neg_lo:[0,1] neg_hi:[0,1]
	v_mov_b32_e32 v13, v169
	v_xor_b32_e32 v36, 0x80000000, v21
	v_mov_b32_e32 v37, v20
	s_mov_b32 s9, 0x9000
	v_pk_mul_f32 v[36:37], v[36:37], v[52:53] op_sel_hi:[1,0] neg_lo:[0,1] neg_hi:[0,1]
	v_mov_b32_e32 v13, v171
	v_pk_fma_f32 v[20:21], v[20:21], v[10:11], v[36:37] op_sel_hi:[1,0,1]
	s_waitcnt lgkmcnt(5)
	v_pk_add_f32 v[36:37], v[22:23], v[38:39]
	v_pk_add_f32 v[22:23], v[22:23], v[38:39] neg_lo:[0,1] neg_hi:[0,1]
	s_mov_b32 s5, 0xb000
	v_xor_b32_e32 v38, 0x80000000, v23
	v_mov_b32_e32 v39, v22
	v_pk_mul_f32 v[38:39], v[38:39], v[50:51] op_sel_hi:[1,0] neg_lo:[0,1] neg_hi:[0,1]
	v_mov_b32_e32 v13, v172
	v_pk_fma_f32 v[22:23], v[22:23], v[50:51], v[38:39] op_sel_hi:[1,0,1]
	s_waitcnt lgkmcnt(4)
	v_pk_add_f32 v[38:39], v[24:25], v[40:41]
	v_pk_add_f32 v[24:25], v[24:25], v[40:41] neg_lo:[0,1] neg_hi:[0,1]
	s_mov_b32 s6, 0xc000
	v_pk_mul_f32 v[40:41], v[24:25], v[52:53] op_sel_hi:[1,0]
	v_xor_b32_e32 v56, 0x80000000, v25
	v_mov_b32_e32 v57, v24
	v_pk_fma_f32 v[24:25], v[56:57], v[10:11], v[40:41] op_sel_hi:[1,0,1] neg_lo:[0,1,0] neg_hi:[0,1,0]
	s_waitcnt lgkmcnt(3)
	v_pk_add_f32 v[40:41], v[26:27], v[42:43]
	v_pk_add_f32 v[26:27], v[26:27], v[42:43] neg_lo:[0,1] neg_hi:[0,1]
	s_mov_b32 s4, 0xd000
	v_xor_b32_e32 v43, 0x80000000, v26
	v_mov_b32_e32 v42, v27
	s_waitcnt lgkmcnt(2)
	v_pk_add_f32 v[26:27], v[28:29], v[44:45]
	v_pk_add_f32 v[28:29], v[28:29], v[44:45] neg_lo:[0,1] neg_hi:[0,1]
	s_nop 0
	v_pk_mul_f32 v[44:45], v[28:29], v[52:53] op_sel_hi:[1,0] neg_lo:[0,1] neg_hi:[0,1]
	v_xor_b32_e32 v56, 0x80000000, v29
	v_mov_b32_e32 v57, v28
	v_pk_fma_f32 v[28:29], v[56:57], v[10:11], v[44:45] op_sel_hi:[1,0,1] neg_lo:[0,1,0] neg_hi:[0,1,0]
	s_waitcnt lgkmcnt(1)
	v_pk_add_f32 v[44:45], v[30:31], v[46:47]
	v_pk_add_f32 v[30:31], v[30:31], v[46:47] neg_lo:[0,1] neg_hi:[0,1]
	s_nop 0
	v_xor_b32_e32 v46, 0x80000000, v31
	v_mov_b32_e32 v47, v30
	v_pk_mul_f32 v[46:47], v[46:47], v[50:51] op_sel_hi:[1,0] neg_lo:[0,1] neg_hi:[0,1]
	s_nop 0
	v_pk_fma_f32 v[30:31], v[30:31], v[50:51], v[46:47] op_sel_hi:[1,0,1] neg_lo:[0,1,0] neg_hi:[0,1,0]
	s_waitcnt lgkmcnt(0)
	v_pk_add_f32 v[46:47], v[32:33], v[48:49]
	v_pk_add_f32 v[32:33], v[32:33], v[48:49] neg_lo:[0,1] neg_hi:[0,1]
	s_nop 0
	v_xor_b32_e32 v48, 0x80000000, v33
	v_mov_b32_e32 v49, v32
	v_pk_mul_f32 v[48:49], v[48:49], v[52:53] op_sel_hi:[1,0] neg_lo:[0,1] neg_hi:[0,1]
	v_pk_add_f32 v[52:53], v[34:35], v[26:27]
	v_pk_add_f32 v[26:27], v[34:35], v[26:27] neg_lo:[0,1] neg_hi:[0,1]
	v_pk_fma_f32 v[32:33], v[32:33], v[10:11], v[48:49] op_sel_hi:[1,0,1] neg_lo:[0,1,0] neg_hi:[0,1,0]
	v_xor_b32_e32 v34, 0x80000000, v27
	v_mov_b32_e32 v35, v26
	v_pk_mul_f32 v[34:35], v[34:35], v[50:51] op_sel_hi:[1,0] neg_lo:[0,1] neg_hi:[0,1]
	v_pk_add_f32 v[48:49], v[54:55], v[40:41]
	v_pk_fma_f32 v[26:27], v[26:27], v[50:51], v[34:35] op_sel_hi:[1,0,1]
	v_pk_add_f32 v[34:35], v[36:37], v[44:45]
	v_pk_add_f32 v[36:37], v[36:37], v[44:45] neg_lo:[0,1] neg_hi:[0,1]
	v_pk_add_f32 v[40:41], v[54:55], v[40:41] neg_lo:[0,1] neg_hi:[0,1]
	v_xor_b32_e32 v45, 0x80000000, v36
	v_mov_b32_e32 v44, v37
	v_pk_add_f32 v[36:37], v[38:39], v[46:47]
	v_pk_add_f32 v[38:39], v[38:39], v[46:47] neg_lo:[0,1] neg_hi:[0,1]
	v_mov_b32_e32 v10, v164
	v_xor_b32_e32 v46, 0x80000000, v39
	v_mov_b32_e32 v47, v38
	v_pk_mul_f32 v[46:47], v[46:47], v[50:51] op_sel_hi:[1,0] neg_lo:[0,1] neg_hi:[0,1]
	s_nop 0
	v_pk_fma_f32 v[38:39], v[38:39], v[50:51], v[46:47] op_sel_hi:[1,0,1] neg_lo:[0,1,0] neg_hi:[0,1,0]
	v_pk_add_f32 v[46:47], v[48:49], v[34:35]
	v_pk_add_f32 v[34:35], v[48:49], v[34:35] neg_lo:[0,1] neg_hi:[0,1]
	v_pk_add_f32 v[48:49], v[52:53], v[36:37]
	v_pk_add_f32 v[36:37], v[52:53], v[36:37] neg_lo:[0,1] neg_hi:[0,1]
	s_nop 0
	v_xor_b32_e32 v53, 0x80000000, v36
	v_mov_b32_e32 v52, v37
	v_pk_add_f32 v[36:37], v[46:47], v[48:49]
	v_pk_add_f32 v[46:47], v[46:47], v[48:49] neg_lo:[0,1] neg_hi:[0,1]
	v_pk_add_f32 v[48:49], v[34:35], v[52:53]
	v_pk_add_f32 v[34:35], v[34:35], v[52:53] neg_lo:[0,1] neg_hi:[0,1]
	v_pk_add_f32 v[52:53], v[40:41], v[44:45]
	v_pk_add_f32 v[40:41], v[40:41], v[44:45] neg_lo:[0,1] neg_hi:[0,1]
	v_pk_add_f32 v[44:45], v[26:27], v[38:39]
	v_pk_add_f32 v[26:27], v[26:27], v[38:39] neg_lo:[0,1] neg_hi:[0,1]
	s_nop 0
	v_xor_b32_e32 v39, 0x80000000, v26
	v_mov_b32_e32 v38, v27
	v_pk_add_f32 v[26:27], v[52:53], v[44:45]
	v_pk_add_f32 v[44:45], v[52:53], v[44:45] neg_lo:[0,1] neg_hi:[0,1]
	v_pk_add_f32 v[52:53], v[40:41], v[38:39]
	v_pk_add_f32 v[38:39], v[40:41], v[38:39] neg_lo:[0,1] neg_hi:[0,1]
	v_pk_add_f32 v[40:41], v[18:19], v[42:43]
	v_pk_add_f32 v[18:19], v[18:19], v[42:43] neg_lo:[0,1] neg_hi:[0,1]
	v_pk_add_f32 v[42:43], v[20:21], v[28:29]
	v_pk_add_f32 v[20:21], v[20:21], v[28:29] neg_lo:[0,1] neg_hi:[0,1]
	s_nop 0
	v_xor_b32_e32 v28, 0x80000000, v21
	v_mov_b32_e32 v29, v20
	v_pk_mul_f32 v[28:29], v[50:51], v[28:29] op_sel_hi:[0,1] neg_lo:[1,0] neg_hi:[1,0]
	v_pk_fma_f32 v[20:21], v[50:51], v[20:21], v[28:29] op_sel_hi:[0,1,1]
	v_pk_add_f32 v[28:29], v[22:23], v[30:31]
	v_pk_add_f32 v[22:23], v[22:23], v[30:31] neg_lo:[0,1] neg_hi:[0,1]
	s_nop 0
	v_xor_b32_e32 v31, 0x80000000, v22
	v_mov_b32_e32 v30, v23
	v_pk_add_f32 v[22:23], v[24:25], v[32:33]
	v_pk_add_f32 v[24:25], v[24:25], v[32:33] neg_lo:[0,1] neg_hi:[0,1]
	s_nop 0
	v_xor_b32_e32 v32, 0x80000000, v25
	v_mov_b32_e32 v33, v24
	v_pk_mul_f32 v[32:33], v[50:51], v[32:33] op_sel_hi:[0,1] neg_lo:[1,0] neg_hi:[1,0]
	v_pk_fma_f32 v[24:25], v[50:51], v[24:25], v[32:33] op_sel_hi:[0,1,1] neg_lo:[1,0,0] neg_hi:[1,0,0]
	v_pk_add_f32 v[32:33], v[40:41], v[28:29]
	v_pk_add_f32 v[28:29], v[40:41], v[28:29] neg_lo:[0,1] neg_hi:[0,1]
	v_pk_add_f32 v[40:41], v[42:43], v[22:23]
	v_pk_add_f32 v[22:23], v[42:43], v[22:23] neg_lo:[0,1] neg_hi:[0,1]
	s_nop 0
	v_xor_b32_e32 v43, 0x80000000, v22
	v_mov_b32_e32 v42, v23
	v_pk_add_f32 v[22:23], v[32:33], v[40:41]
	v_pk_add_f32 v[32:33], v[32:33], v[40:41] neg_lo:[0,1] neg_hi:[0,1]
	v_pk_add_f32 v[40:41], v[28:29], v[42:43]
	v_pk_add_f32 v[28:29], v[28:29], v[42:43] neg_lo:[0,1] neg_hi:[0,1]
	v_pk_add_f32 v[42:43], v[18:19], v[30:31]
	v_pk_add_f32 v[18:19], v[18:19], v[30:31] neg_lo:[0,1] neg_hi:[0,1]
	v_pk_add_f32 v[30:31], v[20:21], v[24:25]
	v_pk_add_f32 v[20:21], v[20:21], v[24:25] neg_lo:[0,1] neg_hi:[0,1]
	s_nop 0
	v_xor_b32_e32 v25, 0x80000000, v20
	v_mov_b32_e32 v24, v21
	v_pk_add_f32 v[20:21], v[42:43], v[30:31]
	v_pk_add_f32 v[30:31], v[42:43], v[30:31] neg_lo:[0,1] neg_hi:[0,1]
	v_pk_add_f32 v[42:43], v[18:19], v[24:25]
	v_pk_add_f32 v[18:19], v[18:19], v[24:25] neg_lo:[0,1] neg_hi:[0,1]
	v_add_u32_e32 v24, 0x2000, v14
	v_ashrrev_i32_e32 v25, 31, v24
	v_lshl_add_u64 v[24:25], v[24:25], 3, s[48:49]
	global_store_dwordx2 v[24:25], v[36:37], off
	v_add_u32_e32 v24, 0x2200, v14
	v_ashrrev_i32_e32 v25, 31, v24
	v_lshl_add_u64 v[24:25], v[24:25], 3, s[48:49]
	global_store_dwordx2 v[24:25], v[22:23], off
	v_add_u32_e32 v22, 0x2400, v14
	v_ashrrev_i32_e32 v23, 31, v22
	v_lshl_add_u64 v[22:23], v[22:23], 3, s[48:49]
	global_store_dwordx2 v[22:23], v[26:27], off
	v_add_u32_e32 v22, 0x2600, v14
	v_ashrrev_i32_e32 v23, 31, v22
	v_lshl_add_u64 v[22:23], v[22:23], 3, s[48:49]
	global_store_dwordx2 v[22:23], v[20:21], off
	v_add_u32_e32 v20, 0x2800, v14
	v_ashrrev_i32_e32 v21, 31, v20
	v_lshl_add_u64 v[20:21], v[20:21], 3, s[48:49]
	global_store_dwordx2 v[20:21], v[48:49], off
	v_add_u32_e32 v20, 0x2a00, v14
	v_ashrrev_i32_e32 v21, 31, v20
	v_lshl_add_u64 v[20:21], v[20:21], 3, s[48:49]
	global_store_dwordx2 v[20:21], v[40:41], off
	v_add_u32_e32 v20, 0x2c00, v14
	v_ashrrev_i32_e32 v21, 31, v20
	v_lshl_add_u64 v[20:21], v[20:21], 3, s[48:49]
	global_store_dwordx2 v[20:21], v[52:53], off
	v_add_u32_e32 v20, 0x2e00, v14
	v_ashrrev_i32_e32 v21, 31, v20
	v_lshl_add_u64 v[20:21], v[20:21], 3, s[48:49]
	global_store_dwordx2 v[20:21], v[42:43], off
	v_add_u32_e32 v20, 0x3000, v14
	v_ashrrev_i32_e32 v21, 31, v20
	v_lshl_add_u64 v[20:21], v[20:21], 3, s[48:49]
	global_store_dwordx2 v[20:21], v[46:47], off
	v_add_u32_e32 v20, 0x3200, v14
	v_ashrrev_i32_e32 v21, 31, v20
	v_lshl_add_u64 v[20:21], v[20:21], 3, s[48:49]
	global_store_dwordx2 v[20:21], v[32:33], off
	v_add_u32_e32 v20, 0x3400, v14
	v_ashrrev_i32_e32 v21, 31, v20
	v_lshl_add_u64 v[20:21], v[20:21], 3, s[48:49]
	global_store_dwordx2 v[20:21], v[44:45], off
	v_add_u32_e32 v20, 0x3600, v14
	v_ashrrev_i32_e32 v21, 31, v20
	v_lshl_add_u64 v[20:21], v[20:21], 3, s[48:49]
	global_store_dwordx2 v[20:21], v[30:31], off
	v_add_u32_e32 v20, 0x3800, v14
	v_ashrrev_i32_e32 v21, 31, v20
	v_lshl_add_u64 v[20:21], v[20:21], 3, s[48:49]
	global_store_dwordx2 v[20:21], v[34:35], off
	v_add_u32_e32 v20, 0x3a00, v14
	v_ashrrev_i32_e32 v21, 31, v20
	v_lshl_add_u64 v[20:21], v[20:21], 3, s[48:49]
	global_store_dwordx2 v[20:21], v[28:29], off
	v_add_u32_e32 v20, 0x3c00, v14
	v_add_u32_e32 v14, 0x3e00, v14
	v_ashrrev_i32_e32 v15, 31, v14
	v_ashrrev_i32_e32 v21, 31, v20
	v_lshl_add_u64 v[14:15], v[14:15], 3, s[48:49]
	v_lshl_add_u64 v[20:21], v[20:21], 3, s[48:49]
	global_store_dwordx2 v[14:15], v[18:19], off
	v_mov_b32_e32 v14, v1
	global_store_dwordx2 v[20:21], v[38:39], off
	s_barrier
	v_mov_b32_e32 v40, v170
	v_ashrrev_i32_e32 v15, 31, v14
	v_lshl_add_u64 v[18:19], v[14:15], 2, s[66:67]
	v_add_co_u32_e32 v28, vcc, s85, v18
	global_load_dword v20, v[18:19], off
	global_load_dword v21, v[18:19], off offset:2048
	v_addc_co_u32_e32 v29, vcc, 0, v19, vcc
	v_add_co_u32_e32 v22, vcc, s84, v18
	v_mov_b32_e32 v15, v174
	s_nop 0
	v_addc_co_u32_e32 v23, vcc, 0, v19, vcc
	v_add_co_u32_e32 v30, vcc, s61, v18
	v_mov_b32_e32 v45, v11
	s_nop 0
	v_addc_co_u32_e32 v31, vcc, 0, v19, vcc
	v_add_co_u32_e32 v32, vcc, s45, v18
	s_nop 1
	v_addc_co_u32_e32 v33, vcc, 0, v19, vcc
	v_add_co_u32_e32 v34, vcc, s88, v18
	global_load_dword v26, v[22:23], off offset:-4096
	global_load_dword v24, v[22:23], off
	global_load_dword v25, v[22:23], off offset:2048
	s_nop 0
	global_load_dword v22, v[32:33], off offset:-4096
	v_addc_co_u32_e32 v35, vcc, 0, v19, vcc
	v_add_co_u32_e32 v36, vcc, s0, v18
	s_mov_b32 s0, 0xa000
	s_nop 0
	v_addc_co_u32_e32 v37, vcc, 0, v19, vcc
	v_add_co_u32_e32 v38, vcc, s0, v18
	s_mov_b32 s0, 0x9000
	s_nop 0
	v_addc_co_u32_e32 v39, vcc, 0, v19, vcc
	global_load_dword v43, v[32:33], off offset:2048
	global_load_dword v46, v[34:35], off offset:-4096
	global_load_dword v48, v[36:37], off
	global_load_dword v49, v[36:37], off offset:2048
	global_load_dword v62, v[34:35], off
	global_load_dword v63, v[34:35], off offset:2048
	s_nop 0
	global_load_dword v34, v[38:39], off offset:-4096
	global_load_dword v64, v[36:37], off offset:-4096
	v_add_co_u32_e32 v36, vcc, s0, v18
	s_mov_b32 s0, 0xb000
	s_nop 0
	v_addc_co_u32_e32 v37, vcc, 0, v19, vcc
	global_load_dword v27, v[28:29], off offset:2048
	global_load_dword v35, v[36:37], off offset:2048
	v_add_co_u32_e32 v28, vcc, s86, v18
	global_load_dword v66, v[38:39], off
	global_load_dword v67, v[38:39], off offset:2048
	v_addc_co_u32_e32 v29, vcc, 0, v19, vcc
	v_add_co_u32_e32 v36, vcc, s0, v18
	s_mov_b32 s0, 0xc000
	s_nop 0
	v_addc_co_u32_e32 v37, vcc, 0, v19, vcc
	v_add_co_u32_e32 v38, vcc, s0, v18
	s_mov_b32 s0, 0xe000
	s_nop 0
	v_addc_co_u32_e32 v39, vcc, 0, v19, vcc
	global_load_dword v68, v[38:39], off offset:-4096
	global_load_dword v23, v[30:31], off offset:2048
	global_load_dword v69, v[36:37], off offset:2048
	v_add_co_u32_e32 v30, vcc, s90, v18
	s_waitcnt vmcnt(11)
	v_sub_f32_e32 v44, v21, v49
	v_addc_co_u32_e32 v31, vcc, 0, v19, vcc
	global_load_dword v47, v[28:29], off offset:2048
	global_load_dword v65, v[30:31], off offset:2048
	global_load_dword v42, v[32:33], off
	s_nop 0
	global_load_dword v30, v[38:39], off
	global_load_dword v31, v[38:39], off offset:2048
	v_add_co_u32_e32 v28, vcc, s0, v18
	s_mov_b32 s0, 0xd000
	s_nop 0
	v_addc_co_u32_e32 v29, vcc, 0, v19, vcc
	global_load_dword v32, v[28:29], off offset:-4096
	v_add_co_u32_e32 v36, vcc, s0, v18
	s_mov_b32 s0, 0xf000
	s_nop 0
	v_addc_co_u32_e32 v37, vcc, 0, v19, vcc
	global_load_dword v33, v[36:37], off offset:2048
	global_load_dword v38, v[28:29], off
	global_load_dword v39, v[28:29], off offset:2048
	v_add_co_u32_e32 v18, vcc, s0, v18
	v_mov_b32_e32 v36, v166
	s_nop 0
	v_addc_co_u32_e32 v19, vcc, 0, v19, vcc
	global_load_dword v70, v[18:19], off
	global_load_dword v71, v[18:19], off offset:2048
	v_mov_b32_e32 v18, v180
	v_mov_b32_e32 v19, v181
	v_mov_b32_e32 v28, v168
	v_mov_b32_e32 v13, v44
	s_nop 0
	v_mov_b32_e32 v10, v172
	v_pk_mul_f32 v[50:51], v[12:13], v[78:79] op_sel_hi:[1,0] neg_lo:[0,1] neg_hi:[0,1]
	s_waitcnt vmcnt(6)
	v_sub_f32_e32 v82, v43, v31
	v_pk_fma_f32 v[44:45], v[44:45], v[72:73], v[50:51] op_sel_hi:[1,0,1]
	v_sub_f32_e32 v50, v26, v34
	v_mov_b32_e32 v13, v50
	v_mov_b32_e32 v51, v11
	v_pk_mul_f32 v[52:53], v[12:13], v[40:41] op_sel_hi:[1,0] neg_lo:[0,1] neg_hi:[0,1]
	v_pk_mul_f32 v[84:85], v[82:83], v[78:79] op_sel_hi:[1,0] neg_lo:[0,1] neg_hi:[0,1]
	v_pk_fma_f32 v[50:51], v[50:51], v[36:37], v[52:53] op_sel_hi:[1,0,1]
	v_sub_f32_e32 v52, v27, v35
	v_mov_b32_e32 v13, v52
	v_mov_b32_e32 v53, v11
	v_pk_mul_f32 v[54:55], v[12:13], v[76:77] op_sel_hi:[1,0] neg_lo:[0,1] neg_hi:[0,1]
	v_sub_f32_e32 v10, v20, v48
	v_pk_fma_f32 v[54:55], v[52:53], v[74:75], v[54:55] op_sel_hi:[1,0,1]
	v_sub_f32_e32 v52, v24, v66
	v_mov_b32_e32 v13, v52
	v_pk_mul_f32 v[56:57], v[12:13], v[28:29] op_sel_hi:[1,0] neg_lo:[0,1] neg_hi:[0,1]
	v_pk_add_f32 v[20:21], v[20:21], v[48:49]
	v_pk_fma_f32 v[56:57], v[52:53], v[28:29], v[56:57] op_sel_hi:[1,0,1]
	v_sub_f32_e32 v52, v25, v67
	v_pk_mul_f32 v[58:59], v[52:53], v[76:77] op_sel_hi:[1,0]
	v_mov_b32_e32 v13, v52
	v_sub_f32_e32 v52, v22, v68
	v_pk_fma_f32 v[60:61], v[12:13], v[74:75], v[58:59] op_sel_hi:[1,0,1] neg_lo:[0,1,0] neg_hi:[0,1,0]
	v_pk_mul_f32 v[58:59], v[52:53], v[40:41] op_sel_hi:[1,0]
	v_mov_b32_e32 v13, v52
	v_sub_f32_e32 v52, v23, v69
	v_pk_fma_f32 v[58:59], v[12:13], v[36:37], v[58:59] op_sel_hi:[1,0,1] neg_lo:[0,1,0] neg_hi:[0,1,0]
	v_pk_mul_f32 v[80:81], v[52:53], v[78:79] op_sel_hi:[1,0]
	v_mov_b32_e32 v13, v52
	v_pk_fma_f32 v[52:53], v[12:13], v[72:73], v[80:81] op_sel_hi:[1,0,1] neg_lo:[0,1,0] neg_hi:[0,1,0]
	v_sub_f32_e32 v13, v42, v30
	v_xor_b32_e32 v81, 0x80000000, v13
	v_mov_b32_e32 v13, v82
	v_pk_fma_f32 v[82:83], v[12:13], v[72:73], v[84:85] op_sel_hi:[1,0,1] neg_lo:[0,1,0] neg_hi:[0,1,0]
	s_waitcnt vmcnt(5)
	v_sub_f32_e32 v84, v46, v32
	v_mov_b32_e32 v85, v11
	v_pk_mul_f32 v[86:87], v[84:85], v[40:41] op_sel_hi:[1,0] neg_lo:[0,1] neg_hi:[0,1]
	v_mov_b32_e32 v13, v84
	v_pk_fma_f32 v[84:85], v[12:13], v[36:37], v[86:87] op_sel_hi:[1,0,1] neg_lo:[0,1,0] neg_hi:[0,1,0]
	s_waitcnt vmcnt(4)
	v_sub_f32_e32 v86, v47, v33
	v_mov_b32_e32 v87, v11
	v_pk_mul_f32 v[88:89], v[86:87], v[76:77] op_sel_hi:[1,0] neg_lo:[0,1] neg_hi:[0,1]
	v_mov_b32_e32 v13, v86
	v_pk_fma_f32 v[86:87], v[12:13], v[74:75], v[88:89] op_sel_hi:[1,0,1] neg_lo:[0,1,0] neg_hi:[0,1,0]
	s_waitcnt vmcnt(3)
	v_sub_f32_e32 v88, v62, v38
	v_mov_b32_e32 v13, v88
	v_mov_b32_e32 v89, v11
	v_pk_mul_f32 v[90:91], v[12:13], v[28:29] op_sel_hi:[1,0] neg_lo:[0,1] neg_hi:[0,1]
	v_pk_add_f32 v[30:31], v[42:43], v[30:31]
	v_pk_fma_f32 v[88:89], v[88:89], v[28:29], v[90:91] op_sel_hi:[1,0,1] neg_lo:[0,1,0] neg_hi:[0,1,0]
	s_waitcnt vmcnt(2)
	v_sub_f32_e32 v90, v63, v39
	v_mov_b32_e32 v13, v90
	v_mov_b32_e32 v91, v11
	v_pk_mul_f32 v[76:77], v[12:13], v[76:77] op_sel_hi:[1,0] neg_lo:[0,1] neg_hi:[0,1]
	v_pk_add_f32 v[42:43], v[20:21], v[30:31] neg_lo:[0,1] neg_hi:[0,1]
	v_pk_fma_f32 v[74:75], v[90:91], v[74:75], v[76:77] op_sel_hi:[1,0,1] neg_lo:[0,1,0] neg_hi:[0,1,0]
	s_waitcnt vmcnt(1)
	v_sub_f32_e32 v76, v64, v70
	v_mov_b32_e32 v13, v76
	v_mov_b32_e32 v77, v11
	v_pk_mul_f32 v[90:91], v[12:13], v[40:41] op_sel_hi:[1,0] neg_lo:[0,1] neg_hi:[0,1]
	v_pk_add_f32 v[26:27], v[26:27], v[34:35]
	v_pk_fma_f32 v[76:77], v[76:77], v[36:37], v[90:91] op_sel_hi:[1,0,1] neg_lo:[0,1,0] neg_hi:[0,1,0]
	s_waitcnt vmcnt(0)
	v_sub_f32_e32 v90, v65, v71
	v_mov_b32_e32 v13, v90
	v_pk_mul_f32 v[78:79], v[12:13], v[78:79] op_sel_hi:[1,0] neg_lo:[0,1] neg_hi:[0,1]
	v_mov_b32_e32 v13, v43
	v_pk_add_f32 v[32:33], v[46:47], v[32:33]
	v_mov_b32_e32 v46, v42
	v_pk_add_f32 v[20:21], v[20:21], v[30:31]
	v_mov_b32_e32 v30, v43
	v_mov_b32_e32 v31, v11
	v_pk_mul_f32 v[42:43], v[12:13], v[40:41] op_sel_hi:[1,0] neg_lo:[0,1] neg_hi:[0,1]
	v_pk_add_f32 v[34:35], v[62:63], v[38:39]
	v_pk_fma_f32 v[62:63], v[30:31], v[36:37], v[42:43] op_sel_hi:[1,0,1]
	v_pk_add_f32 v[30:31], v[26:27], v[32:33] neg_lo:[0,1] neg_hi:[0,1]
	v_pk_add_f32 v[24:25], v[24:25], v[66:67]
	v_mov_b32_e32 v13, v30
	v_mov_b32_e32 v42, v30
	v_pk_mul_f32 v[48:49], v[12:13], v[28:29] op_sel_hi:[1,0] neg_lo:[0,1] neg_hi:[0,1]
	v_pk_add_f32 v[26:27], v[26:27], v[32:33]
	v_mov_b32_e32 v32, v31
	v_mov_b32_e32 v33, v11
	v_mov_b32_e32 v13, v31
	v_pk_add_f32 v[30:31], v[24:25], v[34:35] neg_lo:[0,1] neg_hi:[0,1]
	v_pk_add_f32 v[22:23], v[22:23], v[68:69]
	v_pk_add_f32 v[38:39], v[64:65], v[70:71]
	v_pk_mul_f32 v[32:33], v[32:33], v[40:41] op_sel_hi:[1,0]
	v_pk_add_f32 v[24:25], v[24:25], v[34:35]
	v_mov_b32_e32 v34, v31
	v_mov_b32_e32 v35, v11
	v_pk_fma_f32 v[32:33], v[12:13], v[36:37], v[32:33] op_sel_hi:[1,0,1] neg_lo:[0,1,0] neg_hi:[0,1,0]
	v_xor_b32_e32 v67, 0x80000000, v30
	v_pk_mul_f32 v[34:35], v[34:35], v[40:41] op_sel_hi:[1,0] neg_lo:[0,1] neg_hi:[0,1]
	v_mov_b32_e32 v13, v31
	v_pk_add_f32 v[30:31], v[22:23], v[38:39] neg_lo:[0,1] neg_hi:[0,1]
	v_mov_b32_e32 v43, v11
	v_pk_fma_f32 v[68:69], v[12:13], v[36:37], v[34:35] op_sel_hi:[1,0,1] neg_lo:[0,1,0] neg_hi:[0,1,0]
	v_mov_b32_e32 v13, v30
	v_pk_fma_f32 v[64:65], v[42:43], v[28:29], v[48:49] op_sel_hi:[1,0,1]
	v_mov_b32_e32 v34, v30
	v_mov_b32_e32 v35, v11
	v_pk_mul_f32 v[42:43], v[12:13], v[28:29] op_sel_hi:[1,0] neg_lo:[0,1] neg_hi:[0,1]
	v_mov_b32_e32 v13, v31
	v_pk_fma_f32 v[70:71], v[34:35], v[28:29], v[42:43] op_sel_hi:[1,0,1] neg_lo:[0,1,0] neg_hi:[0,1,0]
	v_mov_b32_e32 v34, v31
	v_pk_mul_f32 v[30:31], v[12:13], v[40:41] op_sel_hi:[1,0] neg_lo:[0,1] neg_hi:[0,1]
	v_pk_add_f32 v[22:23], v[22:23], v[38:39]
	v_pk_fma_f32 v[38:39], v[34:35], v[36:37], v[30:31] op_sel_hi:[1,0,1] neg_lo:[0,1,0] neg_hi:[0,1,0]
	v_pk_add_f32 v[30:31], v[20:21], v[24:25] neg_lo:[0,1] neg_hi:[0,1]
	v_pk_add_f32 v[20:21], v[20:21], v[24:25]
	v_mov_b32_e32 v13, v31
	v_mov_b32_e32 v42, v30
	v_mov_b32_e32 v24, v31
	v_mov_b32_e32 v25, v11
	v_pk_mul_f32 v[30:31], v[12:13], v[28:29] op_sel_hi:[1,0] neg_lo:[0,1] neg_hi:[0,1]
	v_mov_b32_e32 v91, v11
	v_pk_fma_f32 v[30:31], v[24:25], v[28:29], v[30:31] op_sel_hi:[1,0,1]
	v_pk_add_f32 v[24:25], v[26:27], v[22:23] neg_lo:[0,1] neg_hi:[0,1]
	v_pk_fma_f32 v[72:73], v[90:91], v[72:73], v[78:79] op_sel_hi:[1,0,1] neg_lo:[0,1,0] neg_hi:[0,1,0]
	v_mov_b32_e32 v13, v25
	v_xor_b32_e32 v79, 0x80000000, v24
	v_pk_add_f32 v[22:23], v[26:27], v[22:23]
	v_mov_b32_e32 v26, v25
	v_mov_b32_e32 v27, v11
	v_pk_mul_f32 v[24:25], v[12:13], v[28:29] op_sel_hi:[1,0] neg_lo:[0,1] neg_hi:[0,1]
	v_pk_add_f32 v[34:35], v[20:21], v[22:23]
	v_pk_fma_f32 v[26:27], v[26:27], v[28:29], v[24:25] op_sel_hi:[1,0,1] neg_lo:[0,1,0] neg_hi:[0,1,0]
	v_pk_add_f32 v[24:25], v[20:21], v[22:23] neg_lo:[0,1] neg_hi:[0,1]
	v_mov_b32_e32 v43, v11
	v_pk_add_f32 v[20:21], v[24:25], 0 neg_lo:[1,1] neg_hi:[1,1]
	v_mov_b32_e32 v78, v11
	v_mov_b32_e32 v90, v24
	v_mov_b32_e32 v20, v11
	v_pk_add_f32 v[48:49], v[90:91], v[20:21]
	v_pk_add_f32 v[24:25], v[90:91], v[20:21] neg_lo:[0,1] neg_hi:[0,1]
	v_pk_add_f32 v[20:21], v[42:43], v[78:79]
	v_pk_add_f32 v[22:23], v[42:43], v[78:79] neg_lo:[0,1] neg_hi:[0,1]
	v_pk_add_f32 v[42:43], v[30:31], v[26:27]
	v_pk_add_f32 v[26:27], v[30:31], v[26:27] neg_lo:[0,1] neg_hi:[0,1]
	v_mov_b32_e32 v47, v11
	v_mov_b32_e32 v66, v11
	v_xor_b32_e32 v79, 0x80000000, v26
	v_mov_b32_e32 v78, v27
	v_pk_add_f32 v[26:27], v[62:63], v[68:69]
	v_pk_add_f32 v[62:63], v[62:63], v[68:69] neg_lo:[0,1] neg_hi:[0,1]
	v_pk_add_f32 v[90:91], v[20:21], v[42:43]
	v_pk_add_f32 v[30:31], v[20:21], v[42:43] neg_lo:[0,1] neg_hi:[0,1]
	v_pk_add_f32 v[42:43], v[22:23], v[78:79]
	v_pk_add_f32 v[20:21], v[22:23], v[78:79] neg_lo:[0,1] neg_hi:[0,1]
	v_pk_add_f32 v[22:23], v[46:47], v[66:67]
	v_pk_add_f32 v[46:47], v[46:47], v[66:67] neg_lo:[0,1] neg_hi:[0,1]
	v_xor_b32_e32 v66, 0x80000000, v63
	v_mov_b32_e32 v67, v62
	v_pk_mul_f32 v[66:67], v[28:29], v[66:67] op_sel_hi:[0,1] neg_lo:[1,0] neg_hi:[1,0]
	v_pk_fma_f32 v[66:67], v[28:29], v[62:63], v[66:67] op_sel_hi:[0,1,1]
	v_pk_add_f32 v[62:63], v[64:65], v[70:71]
	v_pk_add_f32 v[64:65], v[64:65], v[70:71] neg_lo:[0,1] neg_hi:[0,1]
	v_mov_b32_e32 v80, v11
	v_xor_b32_e32 v69, 0x80000000, v64
	v_mov_b32_e32 v68, v65
	v_pk_add_f32 v[64:65], v[32:33], v[38:39]
	v_pk_add_f32 v[32:33], v[32:33], v[38:39] neg_lo:[0,1] neg_hi:[0,1]
	v_pk_add_f32 v[78:79], v[44:45], v[82:83]
	v_xor_b32_e32 v38, 0x80000000, v33
	v_mov_b32_e32 v39, v32
	v_pk_mul_f32 v[38:39], v[28:29], v[38:39] op_sel_hi:[0,1] neg_lo:[1,0] neg_hi:[1,0]
	v_pk_fma_f32 v[32:33], v[28:29], v[32:33], v[38:39] op_sel_hi:[0,1,1] neg_lo:[1,0,0] neg_hi:[1,0,0]
	v_pk_add_f32 v[38:39], v[22:23], v[62:63]
	v_pk_add_f32 v[22:23], v[22:23], v[62:63] neg_lo:[0,1] neg_hi:[0,1]
	v_pk_add_f32 v[62:63], v[26:27], v[64:65]
	v_pk_add_f32 v[26:27], v[26:27], v[64:65] neg_lo:[0,1] neg_hi:[0,1]
	v_pk_add_f32 v[70:71], v[38:39], v[62:63]
	v_xor_b32_e32 v65, 0x80000000, v26
	v_mov_b32_e32 v64, v27
	v_pk_add_f32 v[38:39], v[38:39], v[62:63] neg_lo:[0,1] neg_hi:[0,1]
	v_pk_add_f32 v[62:63], v[22:23], v[64:65]
	v_pk_add_f32 v[26:27], v[22:23], v[64:65] neg_lo:[0,1] neg_hi:[0,1]
	v_pk_add_f32 v[22:23], v[46:47], v[68:69]
	v_pk_add_f32 v[64:65], v[46:47], v[68:69] neg_lo:[0,1] neg_hi:[0,1]
	v_pk_add_f32 v[46:47], v[66:67], v[32:33]
	v_pk_add_f32 v[32:33], v[66:67], v[32:33] neg_lo:[0,1] neg_hi:[0,1]
	v_pk_add_f32 v[44:45], v[44:45], v[82:83] neg_lo:[0,1] neg_hi:[0,1]
	v_xor_b32_e32 v67, 0x80000000, v32
	v_mov_b32_e32 v66, v33
	v_pk_add_f32 v[68:69], v[22:23], v[46:47]
	v_pk_add_f32 v[32:33], v[22:23], v[46:47] neg_lo:[0,1] neg_hi:[0,1]
	v_pk_add_f32 v[46:47], v[64:65], v[66:67]
	v_pk_add_f32 v[22:23], v[64:65], v[66:67] neg_lo:[0,1] neg_hi:[0,1]
	v_pk_add_f32 v[64:65], v[10:11], v[80:81]
	v_pk_add_f32 v[66:67], v[10:11], v[80:81] neg_lo:[0,1] neg_hi:[0,1]
	v_xor_b32_e32 v80, 0x80000000, v45
	v_mov_b32_e32 v81, v44
	v_pk_mul_f32 v[80:81], v[40:41], v[80:81] op_sel_hi:[0,1] neg_lo:[1,0] neg_hi:[1,0]
	v_pk_fma_f32 v[44:45], v[36:37], v[44:45], v[80:81] op_sel_hi:[0,1,1]
	v_pk_add_f32 v[80:81], v[50:51], v[84:85]
	v_pk_add_f32 v[50:51], v[50:51], v[84:85] neg_lo:[0,1] neg_hi:[0,1]
	v_add_f32_e32 v10, v34, v35
	v_xor_b32_e32 v82, 0x80000000, v51
	v_mov_b32_e32 v83, v50
	v_pk_mul_f32 v[82:83], v[28:29], v[82:83] op_sel_hi:[0,1] neg_lo:[1,0] neg_hi:[1,0]
	v_pk_fma_f32 v[82:83], v[28:29], v[50:51], v[82:83] op_sel_hi:[0,1,1]
	v_pk_add_f32 v[50:51], v[54:55], v[86:87]
	v_pk_add_f32 v[54:55], v[54:55], v[86:87] neg_lo:[0,1] neg_hi:[0,1]
	v_pk_fma_f32 v[16:17], v[10:11], s[42:43], v[16:17] op_sel_hi:[0,1,1]
	v_xor_b32_e32 v84, 0x80000000, v55
	v_mov_b32_e32 v85, v54
	v_pk_mul_f32 v[84:85], v[36:37], v[84:85] op_sel_hi:[0,1] neg_lo:[1,0] neg_hi:[1,0]
	v_pk_fma_f32 v[84:85], v[40:41], v[54:55], v[84:85] op_sel_hi:[0,1,1]
	v_pk_add_f32 v[54:55], v[56:57], v[88:89]
	v_pk_add_f32 v[56:57], v[56:57], v[88:89] neg_lo:[0,1] neg_hi:[0,1]
	v_lshl_add_u32 v13, v15, 3, 0
	v_xor_b32_e32 v87, 0x80000000, v56
	v_mov_b32_e32 v86, v57
	v_pk_add_f32 v[56:57], v[60:61], v[74:75]
	v_pk_add_f32 v[60:61], v[60:61], v[74:75] neg_lo:[0,1] neg_hi:[0,1]
	ds_write_b64 v13, v[16:17]
	v_xor_b32_e32 v74, 0x80000000, v61
	v_mov_b32_e32 v75, v60
	v_pk_mul_f32 v[74:75], v[36:37], v[74:75] op_sel_hi:[0,1] neg_lo:[1,0] neg_hi:[1,0]
	v_pk_fma_f32 v[60:61], v[40:41], v[60:61], v[74:75] op_sel_hi:[0,1,1] neg_lo:[1,0,0] neg_hi:[1,0,0]
	v_pk_add_f32 v[74:75], v[58:59], v[76:77]
	v_pk_add_f32 v[58:59], v[58:59], v[76:77] neg_lo:[0,1] neg_hi:[0,1]
	v_pk_fma_f32 v[16:17], v[18:19], s[92:93], v[18:19] op_sel:[1,0,0] op_sel_hi:[0,1,1]
	v_xor_b32_e32 v76, 0x80000000, v59
	v_mov_b32_e32 v77, v58
	v_pk_mul_f32 v[76:77], v[28:29], v[76:77] op_sel_hi:[0,1] neg_lo:[1,0] neg_hi:[1,0]
	v_pk_fma_f32 v[58:59], v[28:29], v[58:59], v[76:77] op_sel_hi:[0,1,1] neg_lo:[1,0,0] neg_hi:[1,0,0]
	v_pk_add_f32 v[76:77], v[52:53], v[72:73]
	v_pk_add_f32 v[52:53], v[52:53], v[72:73] neg_lo:[0,1] neg_hi:[0,1]
	s_nop 0
	v_xor_b32_e32 v72, 0x80000000, v53
	v_mov_b32_e32 v73, v52
	v_pk_mul_f32 v[40:41], v[40:41], v[72:73] op_sel_hi:[0,1] neg_lo:[1,0] neg_hi:[1,0]
	v_pk_fma_f32 v[52:53], v[36:37], v[52:53], v[40:41] op_sel_hi:[0,1,1] neg_lo:[1,0,0] neg_hi:[1,0,0]
	v_pk_add_f32 v[36:37], v[64:65], v[54:55]
	v_pk_add_f32 v[64:65], v[64:65], v[54:55] neg_lo:[0,1] neg_hi:[0,1]
	v_pk_add_f32 v[54:55], v[78:79], v[56:57] neg_lo:[0,1] neg_hi:[0,1]
	v_pk_add_f32 v[40:41], v[56:57], v[78:79]
	v_xor_b32_e32 v56, 0x80000000, v55
	v_mov_b32_e32 v57, v54
	v_pk_mul_f32 v[56:57], v[28:29], v[56:57] op_sel_hi:[0,1] neg_lo:[1,0] neg_hi:[1,0]
	v_pk_add_f32 v[72:73], v[80:81], v[74:75] neg_lo:[0,1] neg_hi:[0,1]
	v_pk_fma_f32 v[56:57], v[28:29], v[54:55], v[56:57] op_sel_hi:[0,1,1]
	v_pk_add_f32 v[54:55], v[80:81], v[74:75]
	v_xor_b32_e32 v75, 0x80000000, v72
	v_mov_b32_e32 v74, v73
	v_pk_add_f32 v[72:73], v[50:51], v[76:77]
	v_pk_add_f32 v[50:51], v[50:51], v[76:77] neg_lo:[0,1] neg_hi:[0,1]
	s_nop 0
	v_xor_b32_e32 v76, 0x80000000, v51
	v_mov_b32_e32 v77, v50
	v_pk_mul_f32 v[76:77], v[28:29], v[76:77] op_sel_hi:[0,1] neg_lo:[1,0] neg_hi:[1,0]
	v_pk_fma_f32 v[50:51], v[28:29], v[50:51], v[76:77] op_sel_hi:[0,1,1] neg_lo:[1,0,0] neg_hi:[1,0,0]
	v_pk_add_f32 v[76:77], v[36:37], v[54:55]
	v_pk_add_f32 v[36:37], v[36:37], v[54:55] neg_lo:[0,1] neg_hi:[0,1]
	v_pk_add_f32 v[54:55], v[40:41], v[72:73]
	v_pk_add_f32 v[40:41], v[40:41], v[72:73] neg_lo:[0,1] neg_hi:[0,1]
	v_pk_add_f32 v[78:79], v[76:77], v[54:55]
	v_xor_b32_e32 v73, 0x80000000, v40
	v_mov_b32_e32 v72, v41
	v_pk_add_f32 v[54:55], v[76:77], v[54:55] neg_lo:[0,1] neg_hi:[0,1]
	v_pk_add_f32 v[76:77], v[36:37], v[72:73]
	v_pk_add_f32 v[40:41], v[36:37], v[72:73] neg_lo:[0,1] neg_hi:[0,1]
	v_pk_add_f32 v[72:73], v[56:57], v[50:51]
	v_pk_add_f32 v[50:51], v[56:57], v[50:51] neg_lo:[0,1] neg_hi:[0,1]
	v_pk_add_f32 v[36:37], v[64:65], v[74:75]
	v_pk_add_f32 v[64:65], v[64:65], v[74:75] neg_lo:[0,1] neg_hi:[0,1]
	v_xor_b32_e32 v57, 0x80000000, v50
	v_mov_b32_e32 v56, v51
	v_pk_add_f32 v[74:75], v[36:37], v[72:73]
	v_pk_add_f32 v[50:51], v[36:37], v[72:73] neg_lo:[0,1] neg_hi:[0,1]
	v_pk_add_f32 v[72:73], v[64:65], v[56:57]
	v_pk_add_f32 v[36:37], v[64:65], v[56:57] neg_lo:[0,1] neg_hi:[0,1]
	v_pk_add_f32 v[56:57], v[66:67], v[86:87]
	v_pk_add_f32 v[64:65], v[66:67], v[86:87] neg_lo:[0,1] neg_hi:[0,1]
	v_pk_add_f32 v[66:67], v[60:61], v[44:45]
	v_pk_add_f32 v[44:45], v[44:45], v[60:61] neg_lo:[0,1] neg_hi:[0,1]
	s_nop 0
	v_xor_b32_e32 v60, 0x80000000, v45
	v_mov_b32_e32 v61, v44
	v_pk_mul_f32 v[60:61], v[28:29], v[60:61] op_sel_hi:[0,1] neg_lo:[1,0] neg_hi:[1,0]
	v_pk_fma_f32 v[60:61], v[28:29], v[44:45], v[60:61] op_sel_hi:[0,1,1]
	v_pk_add_f32 v[44:45], v[82:83], v[58:59]
	v_pk_add_f32 v[58:59], v[82:83], v[58:59] neg_lo:[0,1] neg_hi:[0,1]
	s_nop 0
	v_xor_b32_e32 v81, 0x80000000, v58
	v_mov_b32_e32 v80, v59
	v_pk_add_f32 v[58:59], v[84:85], v[52:53]
	v_pk_add_f32 v[52:53], v[84:85], v[52:53] neg_lo:[0,1] neg_hi:[0,1]
	s_nop 0
	v_xor_b32_e32 v82, 0x80000000, v53
	v_mov_b32_e32 v83, v52
	v_pk_mul_f32 v[82:83], v[28:29], v[82:83] op_sel_hi:[0,1] neg_lo:[1,0] neg_hi:[1,0]
	v_pk_fma_f32 v[28:29], v[28:29], v[52:53], v[82:83] op_sel_hi:[0,1,1] neg_lo:[1,0,0] neg_hi:[1,0,0]
	v_pk_add_f32 v[52:53], v[56:57], v[44:45]
	v_pk_add_f32 v[44:45], v[56:57], v[44:45] neg_lo:[0,1] neg_hi:[0,1]
	v_pk_add_f32 v[56:57], v[66:67], v[58:59]
	v_pk_add_f32 v[58:59], v[66:67], v[58:59] neg_lo:[0,1] neg_hi:[0,1]
	s_nop 0
	v_xor_b32_e32 v67, 0x80000000, v58
	v_mov_b32_e32 v66, v59
	v_pk_add_f32 v[82:83], v[44:45], v[66:67]
	v_pk_add_f32 v[44:45], v[44:45], v[66:67] neg_lo:[0,1] neg_hi:[0,1]
	v_pk_add_f32 v[66:67], v[60:61], v[28:29]
	v_pk_add_f32 v[28:29], v[60:61], v[28:29] neg_lo:[0,1] neg_hi:[0,1]
	v_pk_add_f32 v[58:59], v[52:53], v[56:57]
	v_pk_add_f32 v[56:57], v[52:53], v[56:57] neg_lo:[0,1] neg_hi:[0,1]
	v_pk_add_f32 v[52:53], v[64:65], v[80:81]
	v_pk_add_f32 v[64:65], v[64:65], v[80:81] neg_lo:[0,1] neg_hi:[0,1]
	v_xor_b32_e32 v61, 0x80000000, v28
	v_mov_b32_e32 v60, v29
	v_pk_add_f32 v[80:81], v[52:53], v[66:67]
	v_pk_add_f32 v[52:53], v[52:53], v[66:67] neg_lo:[0,1] neg_hi:[0,1]
	v_pk_add_f32 v[66:67], v[64:65], v[60:61]
	v_pk_add_f32 v[28:29], v[64:65], v[60:61] neg_lo:[0,1] neg_hi:[0,1]
	v_xor_b32_e32 v60, 0x80000000, v79
	v_mov_b32_e32 v61, v79
	v_pk_mul_f32 v[60:61], v[16:17], v[60:61] op_sel:[1,0] op_sel_hi:[0,1]
	v_pk_fma_f32 v[60:61], v[16:17], v[78:79], v[60:61] op_sel_hi:[1,0,1]
	ds_write_b64 v13, v[60:61] offset:4224
	v_xor_b32_e32 v60, 0x80000000, v17
	v_mov_b32_e32 v61, v17
	v_pk_mul_f32 v[60:61], v[18:19], v[60:61] op_sel:[1,0] op_sel_hi:[0,1]
	v_pk_fma_f32 v[16:17], v[18:19], v[16:17], v[60:61] op_sel_hi:[1,0,1]
	v_xor_b32_e32 v60, 0x80000000, v71
	v_mov_b32_e32 v61, v71
	v_pk_mul_f32 v[60:61], v[16:17], v[60:61] op_sel:[1,0] op_sel_hi:[0,1]
	v_pk_fma_f32 v[60:61], v[16:17], v[70:71], v[60:61] op_sel_hi:[1,0,1]
	ds_write_b64 v13, v[60:61] offset:8448
	v_xor_b32_e32 v60, 0x80000000, v17
	v_mov_b32_e32 v61, v17
	v_pk_mul_f32 v[60:61], v[18:19], v[60:61] op_sel:[1,0] op_sel_hi:[0,1]
	v_pk_fma_f32 v[16:17], v[18:19], v[16:17], v[60:61] op_sel_hi:[1,0,1]
	v_xor_b32_e32 v60, 0x80000000, v59
	v_mov_b32_e32 v61, v59
	v_pk_mul_f32 v[60:61], v[16:17], v[60:61] op_sel:[1,0] op_sel_hi:[0,1]
	v_pk_fma_f32 v[58:59], v[16:17], v[58:59], v[60:61] op_sel_hi:[1,0,1]
	ds_write_b64 v13, v[58:59] offset:12672
	v_xor_b32_e32 v58, 0x80000000, v17
	v_mov_b32_e32 v59, v17
	v_pk_mul_f32 v[58:59], v[18:19], v[58:59] op_sel:[1,0] op_sel_hi:[0,1]
	v_pk_fma_f32 v[16:17], v[18:19], v[16:17], v[58:59] op_sel_hi:[1,0,1]
	v_xor_b32_e32 v58, 0x80000000, v91
	v_mov_b32_e32 v59, v91
	v_pk_mul_f32 v[58:59], v[58:59], v[16:17] op_sel:[0,1] op_sel_hi:[1,0]
	s_nop 0
	v_pk_fma_f32 v[58:59], v[90:91], v[16:17], v[58:59] op_sel_hi:[0,1,1]
	ds_write_b64 v13, v[58:59] offset:16896
	v_xor_b32_e32 v58, 0x80000000, v17
	v_mov_b32_e32 v59, v17
	v_pk_mul_f32 v[58:59], v[18:19], v[58:59] op_sel:[1,0] op_sel_hi:[0,1]
	v_pk_fma_f32 v[16:17], v[18:19], v[16:17], v[58:59] op_sel_hi:[1,0,1]
	v_xor_b32_e32 v58, 0x80000000, v75
	v_mov_b32_e32 v59, v75
	v_pk_mul_f32 v[58:59], v[16:17], v[58:59] op_sel:[1,0] op_sel_hi:[0,1]
	v_pk_fma_f32 v[58:59], v[16:17], v[74:75], v[58:59] op_sel_hi:[1,0,1]
	ds_write_b64 v13, v[58:59] offset:21120
	v_xor_b32_e32 v58, 0x80000000, v17
	v_mov_b32_e32 v59, v17
	v_pk_mul_f32 v[58:59], v[18:19], v[58:59] op_sel:[1,0] op_sel_hi:[0,1]
	v_pk_fma_f32 v[16:17], v[18:19], v[16:17], v[58:59] op_sel_hi:[1,0,1]
	v_xor_b32_e32 v58, 0x80000000, v69
	v_mov_b32_e32 v59, v69
	v_pk_mul_f32 v[58:59], v[58:59], v[16:17] op_sel:[0,1] op_sel_hi:[1,0]
	s_nop 0
	v_pk_fma_f32 v[58:59], v[68:69], v[16:17], v[58:59] op_sel_hi:[0,1,1]
	ds_write_b64 v13, v[58:59] offset:25344
	v_xor_b32_e32 v58, 0x80000000, v17
	v_mov_b32_e32 v59, v17
	v_pk_mul_f32 v[58:59], v[18:19], v[58:59] op_sel:[1,0] op_sel_hi:[0,1]
	v_pk_fma_f32 v[16:17], v[18:19], v[16:17], v[58:59] op_sel_hi:[1,0,1]
	v_xor_b32_e32 v58, 0x80000000, v81
	v_mov_b32_e32 v59, v81
	v_pk_mul_f32 v[58:59], v[58:59], v[16:17] op_sel:[0,1] op_sel_hi:[1,0]
	s_nop 0
	v_pk_fma_f32 v[58:59], v[80:81], v[16:17], v[58:59] op_sel_hi:[0,1,1]
	ds_write_b64 v13, v[58:59] offset:29568
	v_xor_b32_e32 v58, 0x80000000, v17
	v_mov_b32_e32 v59, v17
	v_pk_mul_f32 v[58:59], v[18:19], v[58:59] op_sel:[1,0] op_sel_hi:[0,1]
	v_pk_fma_f32 v[16:17], v[18:19], v[16:17], v[58:59] op_sel_hi:[1,0,1]
	v_xor_b32_e32 v58, 0x80000000, v49
	v_mov_b32_e32 v59, v49
	v_pk_mul_f32 v[58:59], v[58:59], v[16:17] op_sel:[0,1] op_sel_hi:[1,0]
	s_nop 0
	v_pk_fma_f32 v[48:49], v[48:49], v[16:17], v[58:59] op_sel_hi:[0,1,1]
	ds_write_b64 v13, v[48:49] offset:33792
	v_xor_b32_e32 v48, 0x80000000, v17
	v_mov_b32_e32 v49, v17
	v_pk_mul_f32 v[48:49], v[18:19], v[48:49] op_sel:[1,0] op_sel_hi:[0,1]
	v_pk_fma_f32 v[16:17], v[18:19], v[16:17], v[48:49] op_sel_hi:[1,0,1]
	v_xor_b32_e32 v48, 0x80000000, v77
	v_mov_b32_e32 v49, v77
	v_pk_mul_f32 v[48:49], v[48:49], v[16:17] op_sel:[0,1] op_sel_hi:[1,0]
	s_nop 0
	v_pk_fma_f32 v[48:49], v[76:77], v[16:17], v[48:49] op_sel_hi:[0,1,1]
	ds_write_b64 v13, v[48:49] offset:38016
	v_xor_b32_e32 v48, 0x80000000, v17
	v_mov_b32_e32 v49, v17
	v_pk_mul_f32 v[48:49], v[18:19], v[48:49] op_sel:[1,0] op_sel_hi:[0,1]
	v_pk_fma_f32 v[16:17], v[18:19], v[16:17], v[48:49] op_sel_hi:[1,0,1]
	v_xor_b32_e32 v48, 0x80000000, v63
	v_mov_b32_e32 v49, v63
	v_pk_mul_f32 v[48:49], v[48:49], v[16:17] op_sel:[0,1] op_sel_hi:[1,0]
	s_nop 0
	v_pk_fma_f32 v[48:49], v[62:63], v[16:17], v[48:49] op_sel_hi:[0,1,1]
	ds_write_b64 v13, v[48:49] offset:42240
	v_xor_b32_e32 v48, 0x80000000, v17
	v_mov_b32_e32 v49, v17
	v_pk_mul_f32 v[48:49], v[18:19], v[48:49] op_sel:[1,0] op_sel_hi:[0,1]
	v_pk_fma_f32 v[16:17], v[18:19], v[16:17], v[48:49] op_sel_hi:[1,0,1]
	v_xor_b32_e32 v48, 0x80000000, v83
	v_mov_b32_e32 v49, v83
	v_pk_mul_f32 v[48:49], v[48:49], v[16:17] op_sel:[0,1] op_sel_hi:[1,0]
	s_nop 0
	v_pk_fma_f32 v[48:49], v[82:83], v[16:17], v[48:49] op_sel_hi:[0,1,1]
	ds_write_b64 v13, v[48:49] offset:46464
	v_xor_b32_e32 v48, 0x80000000, v17
	v_mov_b32_e32 v49, v17
	v_pk_mul_f32 v[48:49], v[18:19], v[48:49] op_sel:[1,0] op_sel_hi:[0,1]
	v_pk_fma_f32 v[16:17], v[18:19], v[16:17], v[48:49] op_sel_hi:[1,0,1]
	v_xor_b32_e32 v48, 0x80000000, v43
	v_mov_b32_e32 v49, v43
	v_pk_mul_f32 v[48:49], v[48:49], v[16:17] op_sel:[0,1] op_sel_hi:[1,0]
	s_nop 0
	v_pk_fma_f32 v[42:43], v[42:43], v[16:17], v[48:49] op_sel_hi:[0,1,1]
	ds_write_b64 v13, v[42:43] offset:50688
	v_xor_b32_e32 v42, 0x80000000, v17
	v_mov_b32_e32 v43, v17
	v_pk_mul_f32 v[42:43], v[18:19], v[42:43] op_sel:[1,0] op_sel_hi:[0,1]
	v_pk_fma_f32 v[16:17], v[18:19], v[16:17], v[42:43] op_sel_hi:[1,0,1]
	v_xor_b32_e32 v42, 0x80000000, v73
	v_mov_b32_e32 v43, v73
	v_pk_mul_f32 v[42:43], v[42:43], v[16:17] op_sel:[0,1] op_sel_hi:[1,0]
	s_nop 0
	v_pk_fma_f32 v[42:43], v[72:73], v[16:17], v[42:43] op_sel_hi:[0,1,1]
	ds_write_b64 v13, v[42:43] offset:54912
	v_xor_b32_e32 v42, 0x80000000, v17
	v_mov_b32_e32 v43, v17
	v_pk_mul_f32 v[42:43], v[18:19], v[42:43] op_sel:[1,0] op_sel_hi:[0,1]
	v_pk_fma_f32 v[16:17], v[18:19], v[16:17], v[42:43] op_sel_hi:[1,0,1]
	v_xor_b32_e32 v42, 0x80000000, v47
	v_mov_b32_e32 v43, v47
	v_pk_mul_f32 v[42:43], v[42:43], v[16:17] op_sel:[0,1] op_sel_hi:[1,0]
	s_nop 0
	v_pk_fma_f32 v[42:43], v[46:47], v[16:17], v[42:43] op_sel_hi:[0,1,1]
	ds_write_b64 v13, v[42:43] offset:59136
	v_xor_b32_e32 v42, 0x80000000, v17
	v_mov_b32_e32 v43, v17
	v_pk_mul_f32 v[42:43], v[18:19], v[42:43] op_sel:[1,0] op_sel_hi:[0,1]
	v_pk_fma_f32 v[16:17], v[18:19], v[16:17], v[42:43] op_sel_hi:[1,0,1]
	v_xor_b32_e32 v42, 0x80000000, v67
	v_mov_b32_e32 v43, v67
	v_pk_mul_f32 v[42:43], v[42:43], v[16:17] op_sel:[0,1] op_sel_hi:[1,0]
	s_nop 0
	v_pk_fma_f32 v[42:43], v[66:67], v[16:17], v[42:43] op_sel_hi:[0,1,1]
	ds_write_b64 v13, v[42:43] offset:63360
	v_xor_b32_e32 v42, 0x80000000, v17
	v_mov_b32_e32 v43, v17
	v_pk_mul_f32 v[42:43], v[18:19], v[42:43] op_sel:[1,0] op_sel_hi:[0,1]
	v_pk_fma_f32 v[16:17], v[18:19], v[16:17], v[42:43] op_sel_hi:[1,0,1]
	v_sub_f32_e32 v10, v34, v35
	v_pk_mul_f32 v[34:35], v[16:17], s[46:47]
	s_nop 0
	v_pk_fma_f32 v[34:35], v[10:11], v[16:17], v[34:35] op_sel:[0,0,1] op_sel_hi:[0,1,0]
	v_add_u32_e32 v10, 0x10800, v13
	ds_write_b64 v10, v[34:35]
	v_xor_b32_e32 v34, 0x80000000, v17
	v_mov_b32_e32 v35, v17
	v_pk_mul_f32 v[34:35], v[18:19], v[34:35] op_sel:[1,0] op_sel_hi:[0,1]
	v_pk_fma_f32 v[16:17], v[18:19], v[16:17], v[34:35] op_sel_hi:[1,0,1]
	v_xor_b32_e32 v34, 0x80000000, v55
	v_mov_b32_e32 v35, v55
	v_pk_mul_f32 v[34:35], v[34:35], v[16:17] op_sel:[0,1] op_sel_hi:[1,0]
	v_add_u32_e32 v10, 0x11880, v13
	v_pk_fma_f32 v[34:35], v[54:55], v[16:17], v[34:35] op_sel_hi:[0,1,1]
	ds_write_b64 v10, v[34:35]
	v_xor_b32_e32 v34, 0x80000000, v17
	v_mov_b32_e32 v35, v17
	v_pk_mul_f32 v[34:35], v[18:19], v[34:35] op_sel:[1,0] op_sel_hi:[0,1]
	v_pk_fma_f32 v[16:17], v[18:19], v[16:17], v[34:35] op_sel_hi:[1,0,1]
	v_xor_b32_e32 v34, 0x80000000, v39
	v_mov_b32_e32 v35, v39
	v_pk_mul_f32 v[34:35], v[34:35], v[16:17] op_sel:[0,1] op_sel_hi:[1,0]
	v_add_u32_e32 v10, 0x12900, v13
	v_pk_fma_f32 v[34:35], v[38:39], v[16:17], v[34:35] op_sel_hi:[0,1,1]
	ds_write_b64 v10, v[34:35]
	v_xor_b32_e32 v34, 0x80000000, v17
	v_mov_b32_e32 v35, v17
	v_pk_mul_f32 v[34:35], v[18:19], v[34:35] op_sel:[1,0] op_sel_hi:[0,1]
	v_pk_fma_f32 v[16:17], v[18:19], v[16:17], v[34:35] op_sel_hi:[1,0,1]
	v_xor_b32_e32 v34, 0x80000000, v57
	v_mov_b32_e32 v35, v57
	v_pk_mul_f32 v[34:35], v[34:35], v[16:17] op_sel:[0,1] op_sel_hi:[1,0]
	v_add_u32_e32 v10, 0x13980, v13
	v_pk_fma_f32 v[34:35], v[56:57], v[16:17], v[34:35] op_sel_hi:[0,1,1]
	ds_write_b64 v10, v[34:35]
	v_xor_b32_e32 v34, 0x80000000, v17
	v_mov_b32_e32 v35, v17
	v_pk_mul_f32 v[34:35], v[18:19], v[34:35] op_sel:[1,0] op_sel_hi:[0,1]
	v_pk_fma_f32 v[16:17], v[18:19], v[16:17], v[34:35] op_sel_hi:[1,0,1]
	v_xor_b32_e32 v34, 0x80000000, v31
	v_mov_b32_e32 v35, v31
	v_pk_mul_f32 v[34:35], v[34:35], v[16:17] op_sel:[0,1] op_sel_hi:[1,0]
	v_add_u32_e32 v10, 0x14a00, v13
	v_pk_fma_f32 v[30:31], v[30:31], v[16:17], v[34:35] op_sel_hi:[0,1,1]
	ds_write_b64 v10, v[30:31]
	v_xor_b32_e32 v30, 0x80000000, v17
	v_mov_b32_e32 v31, v17
	v_pk_mul_f32 v[30:31], v[18:19], v[30:31] op_sel:[1,0] op_sel_hi:[0,1]
	v_pk_fma_f32 v[16:17], v[18:19], v[16:17], v[30:31] op_sel_hi:[1,0,1]
	v_xor_b32_e32 v30, 0x80000000, v51
	v_mov_b32_e32 v31, v51
	v_pk_mul_f32 v[30:31], v[30:31], v[16:17] op_sel:[0,1] op_sel_hi:[1,0]
	v_add_u32_e32 v10, 0x15a80, v13
	v_pk_fma_f32 v[30:31], v[50:51], v[16:17], v[30:31] op_sel_hi:[0,1,1]
	ds_write_b64 v10, v[30:31]
	v_xor_b32_e32 v30, 0x80000000, v17
	v_mov_b32_e32 v31, v17
	v_pk_mul_f32 v[30:31], v[18:19], v[30:31] op_sel:[1,0] op_sel_hi:[0,1]
	v_pk_fma_f32 v[16:17], v[18:19], v[16:17], v[30:31] op_sel_hi:[1,0,1]
	v_xor_b32_e32 v30, 0x80000000, v33
	v_mov_b32_e32 v31, v33
	v_pk_mul_f32 v[30:31], v[30:31], v[16:17] op_sel:[0,1] op_sel_hi:[1,0]
	v_add_u32_e32 v10, 0x16b00, v13
	v_pk_fma_f32 v[30:31], v[32:33], v[16:17], v[30:31] op_sel_hi:[0,1,1]
	ds_write_b64 v10, v[30:31]
	v_xor_b32_e32 v30, 0x80000000, v17
	v_mov_b32_e32 v31, v17
	v_pk_mul_f32 v[30:31], v[18:19], v[30:31] op_sel:[1,0] op_sel_hi:[0,1]
	v_pk_fma_f32 v[16:17], v[18:19], v[16:17], v[30:31] op_sel_hi:[1,0,1]
	v_xor_b32_e32 v30, 0x80000000, v53
	v_mov_b32_e32 v31, v53
	v_pk_mul_f32 v[30:31], v[30:31], v[16:17] op_sel:[0,1] op_sel_hi:[1,0]
	v_add_u32_e32 v10, 0x17b80, v13
	v_pk_fma_f32 v[30:31], v[52:53], v[16:17], v[30:31] op_sel_hi:[0,1,1]
	ds_write_b64 v10, v[30:31]
	v_xor_b32_e32 v30, 0x80000000, v17
	v_mov_b32_e32 v31, v17
	v_pk_mul_f32 v[30:31], v[18:19], v[30:31] op_sel:[1,0] op_sel_hi:[0,1]
	v_pk_fma_f32 v[16:17], v[18:19], v[16:17], v[30:31] op_sel_hi:[1,0,1]
	v_xor_b32_e32 v30, 0x80000000, v25
	v_mov_b32_e32 v31, v25
	v_pk_mul_f32 v[30:31], v[30:31], v[16:17] op_sel:[0,1] op_sel_hi:[1,0]
	v_add_u32_e32 v10, 0x18c00, v13
	v_pk_fma_f32 v[24:25], v[24:25], v[16:17], v[30:31] op_sel_hi:[0,1,1]
	ds_write_b64 v10, v[24:25]
	v_xor_b32_e32 v24, 0x80000000, v17
	v_mov_b32_e32 v25, v17
	v_pk_mul_f32 v[24:25], v[18:19], v[24:25] op_sel:[1,0] op_sel_hi:[0,1]
	v_pk_fma_f32 v[16:17], v[18:19], v[16:17], v[24:25] op_sel_hi:[1,0,1]
	v_xor_b32_e32 v24, 0x80000000, v41
	v_mov_b32_e32 v25, v41
	v_pk_mul_f32 v[24:25], v[24:25], v[16:17] op_sel:[0,1] op_sel_hi:[1,0]
	v_add_u32_e32 v10, 0x19c80, v13
	v_pk_fma_f32 v[24:25], v[40:41], v[16:17], v[24:25] op_sel_hi:[0,1,1]
	ds_write_b64 v10, v[24:25]
	v_xor_b32_e32 v24, 0x80000000, v17
	v_mov_b32_e32 v25, v17
	v_pk_mul_f32 v[24:25], v[18:19], v[24:25] op_sel:[1,0] op_sel_hi:[0,1]
	v_pk_fma_f32 v[16:17], v[18:19], v[16:17], v[24:25] op_sel_hi:[1,0,1]
	v_xor_b32_e32 v24, 0x80000000, v27
	v_mov_b32_e32 v25, v27
	v_pk_mul_f32 v[24:25], v[24:25], v[16:17] op_sel:[0,1] op_sel_hi:[1,0]
	v_add_u32_e32 v10, 0x1ad00, v13
	v_pk_fma_f32 v[24:25], v[26:27], v[16:17], v[24:25] op_sel_hi:[0,1,1]
	ds_write_b64 v10, v[24:25]
	v_xor_b32_e32 v24, 0x80000000, v17
	v_mov_b32_e32 v25, v17
	v_pk_mul_f32 v[24:25], v[18:19], v[24:25] op_sel:[1,0] op_sel_hi:[0,1]
	v_pk_fma_f32 v[16:17], v[18:19], v[16:17], v[24:25] op_sel_hi:[1,0,1]
	v_xor_b32_e32 v24, 0x80000000, v45
	v_mov_b32_e32 v25, v45
	v_pk_mul_f32 v[24:25], v[24:25], v[16:17] op_sel:[0,1] op_sel_hi:[1,0]
	v_add_u32_e32 v10, 0x1bd80, v13
	v_pk_fma_f32 v[24:25], v[44:45], v[16:17], v[24:25] op_sel_hi:[0,1,1]
	ds_write_b64 v10, v[24:25]
	v_xor_b32_e32 v24, 0x80000000, v17
	v_mov_b32_e32 v25, v17
	v_pk_mul_f32 v[24:25], v[18:19], v[24:25] op_sel:[1,0] op_sel_hi:[0,1]
	v_pk_fma_f32 v[16:17], v[18:19], v[16:17], v[24:25] op_sel_hi:[1,0,1]
	v_xor_b32_e32 v24, 0x80000000, v21
	v_mov_b32_e32 v25, v21
	v_pk_mul_f32 v[24:25], v[24:25], v[16:17] op_sel:[0,1] op_sel_hi:[1,0]
	v_add_u32_e32 v10, 0x1ce00, v13
	v_pk_fma_f32 v[20:21], v[20:21], v[16:17], v[24:25] op_sel_hi:[0,1,1]
	ds_write_b64 v10, v[20:21]
	v_xor_b32_e32 v20, 0x80000000, v17
	v_mov_b32_e32 v21, v17
	v_pk_mul_f32 v[20:21], v[18:19], v[20:21] op_sel:[1,0] op_sel_hi:[0,1]
	v_pk_fma_f32 v[16:17], v[18:19], v[16:17], v[20:21] op_sel_hi:[1,0,1]
	v_xor_b32_e32 v20, 0x80000000, v37
	v_mov_b32_e32 v21, v37
	v_pk_mul_f32 v[20:21], v[20:21], v[16:17] op_sel:[0,1] op_sel_hi:[1,0]
	v_add_u32_e32 v10, 0x1de80, v13
	v_pk_fma_f32 v[20:21], v[36:37], v[16:17], v[20:21] op_sel_hi:[0,1,1]
	ds_write_b64 v10, v[20:21]
	v_xor_b32_e32 v20, 0x80000000, v17
	v_mov_b32_e32 v21, v17
	v_pk_mul_f32 v[20:21], v[18:19], v[20:21] op_sel:[1,0] op_sel_hi:[0,1]
	v_pk_fma_f32 v[16:17], v[18:19], v[16:17], v[20:21] op_sel_hi:[1,0,1]
	v_xor_b32_e32 v20, 0x80000000, v23
	v_mov_b32_e32 v21, v23
	v_pk_mul_f32 v[20:21], v[20:21], v[16:17] op_sel:[0,1] op_sel_hi:[1,0]
	v_add_u32_e32 v10, 0x1ef00, v13
	v_pk_fma_f32 v[20:21], v[22:23], v[16:17], v[20:21] op_sel_hi:[0,1,1]
	ds_write_b64 v10, v[20:21]
	v_xor_b32_e32 v20, 0x80000000, v17
	v_mov_b32_e32 v21, v17
	v_pk_mul_f32 v[20:21], v[18:19], v[20:21] op_sel:[1,0] op_sel_hi:[0,1]
	v_pk_fma_f32 v[16:17], v[18:19], v[16:17], v[20:21] op_sel_hi:[1,0,1]
	v_xor_b32_e32 v18, 0x80000000, v29
	v_mov_b32_e32 v19, v29
	v_pk_mul_f32 v[18:19], v[18:19], v[16:17] op_sel:[0,1] op_sel_hi:[1,0]
	v_add_u32_e32 v10, 0x1ff80, v13
	v_pk_fma_f32 v[16:17], v[28:29], v[16:17], v[18:19] op_sel_hi:[0,1,1]
	ds_write_b64 v10, v[16:17]
	v_mov_b32_e32 v10, v176
	v_mov_b32_e32 v13, v173
	s_waitcnt lgkmcnt(0)
	s_barrier
	v_mov_b32_e32 v16, v182
	v_add_u32_e32 v15, v13, v10
	v_lshl_add_u32 v75, v15, 3, 0
	v_xad_u32 v15, v13, 1, v10
	v_lshl_add_u32 v74, v15, 3, 0
	v_xad_u32 v15, v13, 2, v10
	v_lshl_add_u32 v73, v15, 3, 0
	v_xad_u32 v15, v13, 3, v10
	v_lshl_add_u32 v72, v15, 3, 0
	v_xad_u32 v15, v13, 4, v10
	v_lshl_add_u32 v71, v15, 3, 0
	v_xad_u32 v15, v13, 5, v10
	v_lshl_add_u32 v70, v15, 3, 0
	v_xad_u32 v15, v13, 6, v10
	v_lshl_add_u32 v69, v15, 3, 0
	v_xad_u32 v15, v13, 7, v10
	v_lshl_add_u32 v68, v15, 3, 0
	v_xad_u32 v15, v13, 8, v10
	v_lshl_add_u32 v15, v15, 3, 0
	v_add_u32_e32 v67, 0x800, v15
	v_xad_u32 v15, v13, 9, v10
	v_lshl_add_u32 v15, v15, 3, 0
	v_add_u32_e32 v66, 0x800, v15
	v_xad_u32 v15, v13, 10, v10
	v_lshl_add_u32 v15, v15, 3, 0
	v_add_u32_e32 v65, 0x800, v15
	v_xad_u32 v15, v13, 11, v10
	v_lshl_add_u32 v15, v15, 3, 0
	v_add_u32_e32 v64, 0x800, v15
	v_xad_u32 v15, v13, 12, v10
	v_mov_b32_e32 v17, v183
	v_lshl_add_u32 v15, v15, 3, 0
	ds_read2_b64 v[18:21], v75 offset1:16
	ds_read2_b64 v[40:43], v67 offset1:16
	v_add_u32_e32 v63, 0x800, v15
	v_xad_u32 v15, v13, 13, v10
	v_lshl_add_u32 v15, v15, 3, 0
	v_add_u32_e32 v62, 0x800, v15
	v_xad_u32 v15, v13, 14, v10
	v_xad_u32 v10, v13, 15, v10
	ds_read2_b64 v[22:25], v74 offset0:32 offset1:48
	ds_read2_b64 v[48:51], v66 offset0:32 offset1:48
	v_lshl_add_u32 v15, v15, 3, 0
	v_lshl_add_u32 v10, v10, 3, 0
	v_add_u32_e32 v15, 0x800, v15
	v_add_u32_e32 v13, 0x800, v10
	v_mov_b32_e32 v10, v164
	ds_read2_b64 v[26:29], v73 offset0:64 offset1:80
	ds_read2_b64 v[58:61], v72 offset0:96 offset1:112
	ds_read2_b64 v[76:79], v71 offset0:128 offset1:144
	ds_read2_b64 v[80:83], v70 offset0:160 offset1:176
	ds_read2_b64 v[84:87], v69 offset0:192 offset1:208
	ds_read2_b64 v[88:91], v68 offset0:224 offset1:240
	ds_read2_b64 v[54:57], v65 offset0:64 offset1:80
	ds_read2_b64 v[92:95], v64 offset0:96 offset1:112
	ds_read2_b64 v[96:99], v63 offset0:128 offset1:144
	ds_read2_b64 v[100:103], v62 offset0:160 offset1:176
	ds_read2_b64 v[104:107], v15 offset0:192 offset1:208
	ds_read2_b64 v[108:111], v13 offset0:224 offset1:240
	s_waitcnt lgkmcnt(14)
	v_pk_add_f32 v[112:113], v[18:19], v[40:41]
	v_pk_add_f32 v[40:41], v[18:19], v[40:41] neg_lo:[0,1] neg_hi:[0,1]
	v_pk_add_f32 v[18:19], v[20:21], v[42:43]
	v_pk_add_f32 v[20:21], v[20:21], v[42:43] neg_lo:[0,1] neg_hi:[0,1]
	v_mov_b32_e32 v30, v165
	v_mov_b32_e32 v32, v166
	v_mov_b32_e32 v34, v167
	v_mov_b32_e32 v10, v168
	v_mov_b32_e32 v38, v169
	v_mov_b32_e32 v36, v170
	v_mov_b32_e32 v46, v171
	v_xor_b32_e32 v42, 0x80000000, v21
	v_mov_b32_e32 v43, v20
	v_mov_b32_e32 v31, v172
	v_pk_mul_f32 v[42:43], v[42:43], v[46:47] op_sel_hi:[1,0] neg_lo:[0,1] neg_hi:[0,1]
	s_nop 0
	v_pk_fma_f32 v[44:45], v[20:21], v[30:31], v[42:43] op_sel_hi:[1,0,1]
	s_waitcnt lgkmcnt(12)
	v_pk_add_f32 v[20:21], v[22:23], v[48:49]
	v_pk_add_f32 v[22:23], v[22:23], v[48:49] neg_lo:[0,1] neg_hi:[0,1]
	s_nop 0
	v_xor_b32_e32 v42, 0x80000000, v23
	v_mov_b32_e32 v43, v22
	v_pk_mul_f32 v[42:43], v[42:43], v[36:37] op_sel_hi:[1,0] neg_lo:[0,1] neg_hi:[0,1]
	s_nop 0
	v_pk_fma_f32 v[48:49], v[22:23], v[32:33], v[42:43] op_sel_hi:[1,0,1]
	v_pk_add_f32 v[22:23], v[24:25], v[50:51]
	v_pk_add_f32 v[24:25], v[24:25], v[50:51] neg_lo:[0,1] neg_hi:[0,1]
	s_nop 0
	v_xor_b32_e32 v42, 0x80000000, v25
	v_mov_b32_e32 v43, v24
	v_pk_mul_f32 v[42:43], v[42:43], v[38:39] op_sel_hi:[1,0] neg_lo:[0,1] neg_hi:[0,1]
	s_nop 0
	v_pk_fma_f32 v[52:53], v[24:25], v[34:35], v[42:43] op_sel_hi:[1,0,1]
	s_waitcnt lgkmcnt(5)
	v_pk_add_f32 v[24:25], v[26:27], v[54:55]
	v_pk_add_f32 v[26:27], v[26:27], v[54:55] neg_lo:[0,1] neg_hi:[0,1]
	s_nop 0
	v_xor_b32_e32 v42, 0x80000000, v27
	v_mov_b32_e32 v43, v26
	v_pk_mul_f32 v[42:43], v[42:43], v[10:11] op_sel_hi:[1,0] neg_lo:[0,1] neg_hi:[0,1]
	s_nop 0
	v_pk_fma_f32 v[54:55], v[26:27], v[10:11], v[42:43] op_sel_hi:[1,0,1]
	v_pk_add_f32 v[26:27], v[28:29], v[56:57]
	v_pk_add_f32 v[28:29], v[28:29], v[56:57] neg_lo:[0,1] neg_hi:[0,1]
	s_nop 0
	v_pk_mul_f32 v[42:43], v[28:29], v[38:39] op_sel_hi:[1,0]
	v_xor_b32_e32 v50, 0x80000000, v29
	v_mov_b32_e32 v51, v28
	v_pk_fma_f32 v[56:57], v[50:51], v[34:35], v[42:43] op_sel_hi:[1,0,1] neg_lo:[0,1,0] neg_hi:[0,1,0]
	s_waitcnt lgkmcnt(4)
	v_pk_add_f32 v[42:43], v[58:59], v[92:93] neg_lo:[0,1] neg_hi:[0,1]
	v_pk_add_f32 v[28:29], v[58:59], v[92:93]
	v_pk_mul_f32 v[50:51], v[42:43], v[36:37] op_sel_hi:[1,0]
	v_xor_b32_e32 v58, 0x80000000, v43
	v_mov_b32_e32 v59, v42
	v_pk_fma_f32 v[58:59], v[58:59], v[32:33], v[50:51] op_sel_hi:[1,0,1] neg_lo:[0,1,0] neg_hi:[0,1,0]
	v_pk_add_f32 v[50:51], v[60:61], v[94:95] neg_lo:[0,1] neg_hi:[0,1]
	v_pk_add_f32 v[42:43], v[60:61], v[94:95]
	v_pk_mul_f32 v[60:61], v[50:51], v[46:47] op_sel_hi:[1,0]
	v_xor_b32_e32 v92, 0x80000000, v51
	v_mov_b32_e32 v93, v50
	s_waitcnt lgkmcnt(3)
	v_pk_add_f32 v[50:51], v[76:77], v[96:97]
	v_pk_add_f32 v[76:77], v[76:77], v[96:97] neg_lo:[0,1] neg_hi:[0,1]
	v_pk_fma_f32 v[60:61], v[92:93], v[30:31], v[60:61] op_sel_hi:[1,0,1] neg_lo:[0,1,0] neg_hi:[0,1,0]
	v_xor_b32_e32 v93, 0x80000000, v76
	v_mov_b32_e32 v92, v77
	v_pk_add_f32 v[76:77], v[78:79], v[98:99]
	v_pk_add_f32 v[78:79], v[78:79], v[98:99] neg_lo:[0,1] neg_hi:[0,1]
	s_nop 0
	v_pk_mul_f32 v[94:95], v[78:79], v[46:47] op_sel_hi:[1,0] neg_lo:[0,1] neg_hi:[0,1]
	v_xor_b32_e32 v96, 0x80000000, v79
	v_mov_b32_e32 v97, v78
	v_pk_fma_f32 v[78:79], v[96:97], v[30:31], v[94:95] op_sel_hi:[1,0,1] neg_lo:[0,1,0] neg_hi:[0,1,0]
	s_waitcnt lgkmcnt(2)
	v_pk_add_f32 v[94:95], v[80:81], v[100:101]
	v_pk_add_f32 v[80:81], v[80:81], v[100:101] neg_lo:[0,1] neg_hi:[0,1]
	s_nop 0
	v_pk_mul_f32 v[96:97], v[80:81], v[36:37] op_sel_hi:[1,0] neg_lo:[0,1] neg_hi:[0,1]
	v_xor_b32_e32 v98, 0x80000000, v81
	v_mov_b32_e32 v99, v80
	v_pk_fma_f32 v[80:81], v[98:99], v[32:33], v[96:97] op_sel_hi:[1,0,1] neg_lo:[0,1,0] neg_hi:[0,1,0]
	v_pk_add_f32 v[96:97], v[82:83], v[102:103]
	v_pk_add_f32 v[82:83], v[82:83], v[102:103] neg_lo:[0,1] neg_hi:[0,1]
	s_nop 0
	v_pk_mul_f32 v[98:99], v[82:83], v[38:39] op_sel_hi:[1,0] neg_lo:[0,1] neg_hi:[0,1]
	v_xor_b32_e32 v100, 0x80000000, v83
	v_mov_b32_e32 v101, v82
	v_pk_fma_f32 v[82:83], v[100:101], v[34:35], v[98:99] op_sel_hi:[1,0,1] neg_lo:[0,1,0] neg_hi:[0,1,0]
	s_waitcnt lgkmcnt(1)
	v_pk_add_f32 v[98:99], v[84:85], v[104:105]
	v_pk_add_f32 v[84:85], v[84:85], v[104:105] neg_lo:[0,1] neg_hi:[0,1]
	s_nop 0
	v_xor_b32_e32 v100, 0x80000000, v85
	v_mov_b32_e32 v101, v84
	v_pk_mul_f32 v[100:101], v[100:101], v[10:11] op_sel_hi:[1,0] neg_lo:[0,1] neg_hi:[0,1]
	s_nop 0
	v_pk_fma_f32 v[84:85], v[84:85], v[10:11], v[100:101] op_sel_hi:[1,0,1] neg_lo:[0,1,0] neg_hi:[0,1,0]
	v_pk_add_f32 v[100:101], v[86:87], v[106:107]
	v_pk_add_f32 v[86:87], v[86:87], v[106:107] neg_lo:[0,1] neg_hi:[0,1]
	s_nop 0
	v_xor_b32_e32 v102, 0x80000000, v87
	v_mov_b32_e32 v103, v86
	v_pk_mul_f32 v[38:39], v[102:103], v[38:39] op_sel_hi:[1,0] neg_lo:[0,1] neg_hi:[0,1]
	s_nop 0
	v_pk_fma_f32 v[86:87], v[86:87], v[34:35], v[38:39] op_sel_hi:[1,0,1] neg_lo:[0,1,0] neg_hi:[0,1,0]
	s_waitcnt lgkmcnt(0)
	v_pk_add_f32 v[38:39], v[88:89], v[108:109] neg_lo:[0,1] neg_hi:[0,1]
	v_pk_add_f32 v[34:35], v[88:89], v[108:109]
	v_xor_b32_e32 v88, 0x80000000, v39
	v_mov_b32_e32 v89, v38
	v_pk_mul_f32 v[88:89], v[88:89], v[36:37] op_sel_hi:[1,0] neg_lo:[0,1] neg_hi:[0,1]
	s_nop 0
	v_pk_fma_f32 v[88:89], v[38:39], v[32:33], v[88:89] op_sel_hi:[1,0,1] neg_lo:[0,1,0] neg_hi:[0,1,0]
	v_pk_add_f32 v[38:39], v[90:91], v[110:111]
	v_pk_add_f32 v[90:91], v[90:91], v[110:111] neg_lo:[0,1] neg_hi:[0,1]
	s_nop 0
	v_xor_b32_e32 v102, 0x80000000, v91
	v_mov_b32_e32 v103, v90
	v_pk_mul_f32 v[46:47], v[102:103], v[46:47] op_sel_hi:[1,0] neg_lo:[0,1] neg_hi:[0,1]
	s_nop 0
	v_pk_fma_f32 v[90:91], v[90:91], v[30:31], v[46:47] op_sel_hi:[1,0,1] neg_lo:[0,1,0] neg_hi:[0,1,0]
	v_pk_add_f32 v[46:47], v[18:19], v[76:77]
	v_pk_add_f32 v[18:19], v[18:19], v[76:77] neg_lo:[0,1] neg_hi:[0,1]
	v_pk_add_f32 v[30:31], v[112:113], v[50:51]
	v_xor_b32_e32 v76, 0x80000000, v19
	v_mov_b32_e32 v77, v18
	v_pk_mul_f32 v[76:77], v[76:77], v[36:37] op_sel_hi:[1,0] neg_lo:[0,1] neg_hi:[0,1]
	v_pk_add_f32 v[50:51], v[112:113], v[50:51] neg_lo:[0,1] neg_hi:[0,1]
	v_pk_fma_f32 v[76:77], v[18:19], v[32:33], v[76:77] op_sel_hi:[1,0,1]
	v_pk_add_f32 v[18:19], v[20:21], v[94:95]
	v_pk_add_f32 v[20:21], v[20:21], v[94:95] neg_lo:[0,1] neg_hi:[0,1]
	s_nop 0
	v_xor_b32_e32 v94, 0x80000000, v21
	v_mov_b32_e32 v95, v20
	v_pk_mul_f32 v[94:95], v[94:95], v[10:11] op_sel_hi:[1,0] neg_lo:[0,1] neg_hi:[0,1]
	s_nop 0
	v_pk_fma_f32 v[20:21], v[20:21], v[10:11], v[94:95] op_sel_hi:[1,0,1]
	v_pk_add_f32 v[94:95], v[22:23], v[96:97]
	v_pk_add_f32 v[22:23], v[22:23], v[96:97] neg_lo:[0,1] neg_hi:[0,1]
	s_nop 0
	v_pk_mul_f32 v[96:97], v[22:23], v[36:37] op_sel_hi:[1,0]
	v_xor_b32_e32 v102, 0x80000000, v23
	v_mov_b32_e32 v103, v22
	v_pk_add_f32 v[22:23], v[24:25], v[98:99]
	v_pk_add_f32 v[24:25], v[24:25], v[98:99] neg_lo:[0,1] neg_hi:[0,1]
	v_pk_fma_f32 v[96:97], v[102:103], v[32:33], v[96:97] op_sel_hi:[1,0,1] neg_lo:[0,1,0] neg_hi:[0,1,0]
	v_xor_b32_e32 v99, 0x80000000, v24
	v_mov_b32_e32 v98, v25
	v_pk_add_f32 v[24:25], v[26:27], v[100:101]
	v_pk_add_f32 v[26:27], v[26:27], v[100:101] neg_lo:[0,1] neg_hi:[0,1]
	s_nop 0
	v_pk_mul_f32 v[100:101], v[26:27], v[36:37] op_sel_hi:[1,0] neg_lo:[0,1] neg_hi:[0,1]
	v_xor_b32_e32 v102, 0x80000000, v27
	v_mov_b32_e32 v103, v26
	v_pk_add_f32 v[26:27], v[28:29], v[34:35]
	v_pk_add_f32 v[28:29], v[28:29], v[34:35] neg_lo:[0,1] neg_hi:[0,1]
	v_pk_fma_f32 v[100:101], v[102:103], v[32:33], v[100:101] op_sel_hi:[1,0,1] neg_lo:[0,1,0] neg_hi:[0,1,0]
	v_xor_b32_e32 v34, 0x80000000, v29
	v_mov_b32_e32 v35, v28
	v_pk_mul_f32 v[34:35], v[34:35], v[10:11] op_sel_hi:[1,0] neg_lo:[0,1] neg_hi:[0,1]
	v_pk_add_f32 v[102:103], v[30:31], v[22:23] neg_lo:[0,1] neg_hi:[0,1]
	v_pk_fma_f32 v[28:29], v[28:29], v[10:11], v[34:35] op_sel_hi:[1,0,1] neg_lo:[0,1,0] neg_hi:[0,1,0]
	v_pk_add_f32 v[34:35], v[42:43], v[38:39]
	v_pk_add_f32 v[38:39], v[42:43], v[38:39] neg_lo:[0,1] neg_hi:[0,1]
	s_nop 0
	v_xor_b32_e32 v42, 0x80000000, v39
	v_mov_b32_e32 v43, v38
	v_pk_mul_f32 v[42:43], v[42:43], v[36:37] op_sel_hi:[1,0] neg_lo:[0,1] neg_hi:[0,1]
	s_nop 0
	v_pk_fma_f32 v[42:43], v[38:39], v[32:33], v[42:43] op_sel_hi:[1,0,1] neg_lo:[0,1,0] neg_hi:[0,1,0]
	v_pk_add_f32 v[38:39], v[30:31], v[22:23]
	v_pk_add_f32 v[22:23], v[46:47], v[24:25]
	v_pk_add_f32 v[24:25], v[46:47], v[24:25] neg_lo:[0,1] neg_hi:[0,1]
	s_nop 0
	v_xor_b32_e32 v30, 0x80000000, v25
	v_mov_b32_e32 v31, v24
	v_pk_mul_f32 v[30:31], v[30:31], v[10:11] op_sel_hi:[1,0] neg_lo:[0,1] neg_hi:[0,1]
	s_nop 0
	v_pk_fma_f32 v[24:25], v[24:25], v[10:11], v[30:31] op_sel_hi:[1,0,1]
	v_pk_add_f32 v[30:31], v[18:19], v[26:27]
	v_pk_add_f32 v[18:19], v[18:19], v[26:27] neg_lo:[0,1] neg_hi:[0,1]
	s_nop 0
	v_xor_b32_e32 v27, 0x80000000, v18
	v_mov_b32_e32 v26, v19
	v_pk_add_f32 v[18:19], v[94:95], v[34:35]
	v_pk_add_f32 v[34:35], v[94:95], v[34:35] neg_lo:[0,1] neg_hi:[0,1]
	s_nop 0
	v_xor_b32_e32 v46, 0x80000000, v35
	v_mov_b32_e32 v47, v34
	v_pk_mul_f32 v[46:47], v[46:47], v[10:11] op_sel_hi:[1,0] neg_lo:[0,1] neg_hi:[0,1]
	s_nop 0
	v_pk_fma_f32 v[34:35], v[34:35], v[10:11], v[46:47] op_sel_hi:[1,0,1] neg_lo:[0,1,0] neg_hi:[0,1,0]
	v_pk_add_f32 v[46:47], v[38:39], v[30:31]
	v_pk_add_f32 v[38:39], v[38:39], v[30:31] neg_lo:[0,1] neg_hi:[0,1]
	v_pk_add_f32 v[30:31], v[22:23], v[18:19]
	v_pk_add_f32 v[18:19], v[22:23], v[18:19] neg_lo:[0,1] neg_hi:[0,1]
	v_pk_add_f32 v[94:95], v[46:47], v[30:31]
	v_xor_b32_e32 v23, 0x80000000, v18
	v_mov_b32_e32 v22, v19
	v_pk_add_f32 v[18:19], v[102:103], v[26:27]
	v_pk_add_f32 v[102:103], v[102:103], v[26:27] neg_lo:[0,1] neg_hi:[0,1]
	v_pk_add_f32 v[26:27], v[24:25], v[34:35]
	v_pk_add_f32 v[24:25], v[24:25], v[34:35] neg_lo:[0,1] neg_hi:[0,1]
	v_pk_add_f32 v[30:31], v[46:47], v[30:31] neg_lo:[0,1] neg_hi:[0,1]
	v_xor_b32_e32 v35, 0x80000000, v24
	v_mov_b32_e32 v34, v25
	v_pk_add_f32 v[24:25], v[50:51], v[98:99]
	v_pk_add_f32 v[98:99], v[50:51], v[98:99] neg_lo:[0,1] neg_hi:[0,1]
	v_pk_add_f32 v[50:51], v[76:77], v[100:101] neg_lo:[0,1] neg_hi:[0,1]
	v_pk_add_f32 v[46:47], v[38:39], v[22:23]
	v_pk_add_f32 v[22:23], v[38:39], v[22:23] neg_lo:[0,1] neg_hi:[0,1]
	v_pk_add_f32 v[104:105], v[18:19], v[26:27]
	v_pk_add_f32 v[26:27], v[18:19], v[26:27] neg_lo:[0,1] neg_hi:[0,1]
	v_pk_add_f32 v[38:39], v[102:103], v[34:35]
	v_pk_add_f32 v[18:19], v[102:103], v[34:35] neg_lo:[0,1] neg_hi:[0,1]
	v_pk_add_f32 v[34:35], v[76:77], v[100:101]
	v_xor_b32_e32 v76, 0x80000000, v51
	v_mov_b32_e32 v77, v50
	v_pk_mul_f32 v[76:77], v[10:11], v[76:77] op_sel_hi:[0,1] neg_lo:[1,0] neg_hi:[1,0]
	v_pk_fma_f32 v[76:77], v[10:11], v[50:51], v[76:77] op_sel_hi:[0,1,1]
	v_pk_add_f32 v[50:51], v[20:21], v[28:29]
	v_pk_add_f32 v[20:21], v[20:21], v[28:29] neg_lo:[0,1] neg_hi:[0,1]
	s_nop 0
	v_xor_b32_e32 v29, 0x80000000, v20
	v_mov_b32_e32 v28, v21
	v_pk_add_f32 v[20:21], v[96:97], v[42:43]
	v_pk_add_f32 v[42:43], v[96:97], v[42:43] neg_lo:[0,1] neg_hi:[0,1]
	s_nop 0
	v_xor_b32_e32 v96, 0x80000000, v43
	v_mov_b32_e32 v97, v42
	v_pk_mul_f32 v[96:97], v[10:11], v[96:97] op_sel_hi:[0,1] neg_lo:[1,0] neg_hi:[1,0]
	v_pk_fma_f32 v[42:43], v[10:11], v[42:43], v[96:97] op_sel_hi:[0,1,1] neg_lo:[1,0,0] neg_hi:[1,0,0]
	v_pk_add_f32 v[96:97], v[24:25], v[50:51]
	v_pk_add_f32 v[24:25], v[24:25], v[50:51] neg_lo:[0,1] neg_hi:[0,1]
	v_pk_add_f32 v[50:51], v[34:35], v[20:21]
	v_pk_add_f32 v[20:21], v[34:35], v[20:21] neg_lo:[0,1] neg_hi:[0,1]
	v_pk_add_f32 v[102:103], v[96:97], v[50:51]
	v_xor_b32_e32 v101, 0x80000000, v20
	v_mov_b32_e32 v100, v21
	v_pk_add_f32 v[34:35], v[96:97], v[50:51] neg_lo:[0,1] neg_hi:[0,1]
	v_pk_add_f32 v[20:21], v[98:99], v[28:29]
	v_pk_add_f32 v[96:97], v[98:99], v[28:29] neg_lo:[0,1] neg_hi:[0,1]
	v_pk_add_f32 v[28:29], v[76:77], v[42:43]
	v_pk_add_f32 v[42:43], v[76:77], v[42:43] neg_lo:[0,1] neg_hi:[0,1]
	v_pk_add_f32 v[98:99], v[20:21], v[28:29]
	v_xor_b32_e32 v77, 0x80000000, v42
	v_mov_b32_e32 v76, v43
	v_pk_add_f32 v[28:29], v[20:21], v[28:29] neg_lo:[0,1] neg_hi:[0,1]
	v_pk_add_f32 v[42:43], v[96:97], v[76:77]
	v_pk_add_f32 v[20:21], v[96:97], v[76:77] neg_lo:[0,1] neg_hi:[0,1]
	v_pk_add_f32 v[76:77], v[40:41], v[92:93]
	v_pk_add_f32 v[92:93], v[40:41], v[92:93] neg_lo:[0,1] neg_hi:[0,1]
	v_pk_add_f32 v[40:41], v[44:45], v[78:79]
	v_pk_add_f32 v[44:45], v[44:45], v[78:79] neg_lo:[0,1] neg_hi:[0,1]
	v_pk_add_f32 v[50:51], v[24:25], v[100:101]
	v_xor_b32_e32 v78, 0x80000000, v45
	v_mov_b32_e32 v79, v44
	v_pk_mul_f32 v[78:79], v[36:37], v[78:79] op_sel_hi:[0,1] neg_lo:[1,0] neg_hi:[1,0]
	v_pk_fma_f32 v[44:45], v[32:33], v[44:45], v[78:79] op_sel_hi:[0,1,1]
	v_pk_add_f32 v[78:79], v[48:49], v[80:81]
	v_pk_add_f32 v[48:49], v[48:49], v[80:81] neg_lo:[0,1] neg_hi:[0,1]
	v_pk_add_f32 v[24:25], v[24:25], v[100:101] neg_lo:[0,1] neg_hi:[0,1]
	v_xor_b32_e32 v80, 0x80000000, v49
	v_mov_b32_e32 v81, v48
	v_pk_mul_f32 v[80:81], v[10:11], v[80:81] op_sel_hi:[0,1] neg_lo:[1,0] neg_hi:[1,0]
	v_pk_fma_f32 v[80:81], v[10:11], v[48:49], v[80:81] op_sel_hi:[0,1,1]
	v_pk_add_f32 v[48:49], v[52:53], v[82:83]
	v_pk_add_f32 v[52:53], v[52:53], v[82:83] neg_lo:[0,1] neg_hi:[0,1]
	s_nop 0
	v_xor_b32_e32 v82, 0x80000000, v53
	v_mov_b32_e32 v83, v52
	v_pk_mul_f32 v[82:83], v[32:33], v[82:83] op_sel_hi:[0,1] neg_lo:[1,0] neg_hi:[1,0]
	v_pk_fma_f32 v[52:53], v[36:37], v[52:53], v[82:83] op_sel_hi:[0,1,1]
	v_pk_add_f32 v[82:83], v[54:55], v[84:85]
	v_pk_add_f32 v[54:55], v[54:55], v[84:85] neg_lo:[0,1] neg_hi:[0,1]
	s_nop 0
	v_xor_b32_e32 v85, 0x80000000, v54
	v_mov_b32_e32 v84, v55
	v_pk_add_f32 v[54:55], v[56:57], v[86:87]
	v_pk_add_f32 v[56:57], v[56:57], v[86:87] neg_lo:[0,1] neg_hi:[0,1]
	s_nop 0
	v_xor_b32_e32 v86, 0x80000000, v57
	v_mov_b32_e32 v87, v56
	v_pk_mul_f32 v[86:87], v[32:33], v[86:87] op_sel_hi:[0,1] neg_lo:[1,0] neg_hi:[1,0]
	v_pk_fma_f32 v[56:57], v[36:37], v[56:57], v[86:87] op_sel_hi:[0,1,1] neg_lo:[1,0,0] neg_hi:[1,0,0]
	v_pk_add_f32 v[86:87], v[58:59], v[88:89]
	v_pk_add_f32 v[58:59], v[58:59], v[88:89] neg_lo:[0,1] neg_hi:[0,1]
	s_nop 0
	v_xor_b32_e32 v88, 0x80000000, v59
	v_mov_b32_e32 v89, v58
	v_pk_mul_f32 v[88:89], v[10:11], v[88:89] op_sel_hi:[0,1] neg_lo:[1,0] neg_hi:[1,0]
	v_pk_fma_f32 v[58:59], v[10:11], v[58:59], v[88:89] op_sel_hi:[0,1,1] neg_lo:[1,0,0] neg_hi:[1,0,0]
	v_pk_add_f32 v[88:89], v[60:61], v[90:91]
	v_pk_add_f32 v[60:61], v[60:61], v[90:91] neg_lo:[0,1] neg_hi:[0,1]
	s_nop 0
	v_xor_b32_e32 v90, 0x80000000, v61
	v_mov_b32_e32 v91, v60
	v_pk_mul_f32 v[36:37], v[36:37], v[90:91] op_sel_hi:[0,1] neg_lo:[1,0] neg_hi:[1,0]
	v_pk_fma_f32 v[36:37], v[32:33], v[60:61], v[36:37] op_sel_hi:[0,1,1] neg_lo:[1,0,0] neg_hi:[1,0,0]
	v_pk_add_f32 v[32:33], v[76:77], v[82:83]
	v_pk_add_f32 v[60:61], v[76:77], v[82:83] neg_lo:[0,1] neg_hi:[0,1]
	v_pk_add_f32 v[76:77], v[54:55], v[40:41]
	v_pk_add_f32 v[40:41], v[40:41], v[54:55] neg_lo:[0,1] neg_hi:[0,1]
	s_nop 0
	v_xor_b32_e32 v54, 0x80000000, v41
	v_mov_b32_e32 v55, v40
	v_pk_mul_f32 v[54:55], v[10:11], v[54:55] op_sel_hi:[0,1] neg_lo:[1,0] neg_hi:[1,0]
	v_pk_fma_f32 v[54:55], v[10:11], v[40:41], v[54:55] op_sel_hi:[0,1,1]
	v_pk_add_f32 v[40:41], v[78:79], v[86:87]
	v_pk_add_f32 v[78:79], v[78:79], v[86:87] neg_lo:[0,1] neg_hi:[0,1]
	s_nop 0
	v_xor_b32_e32 v83, 0x80000000, v78
	v_mov_b32_e32 v82, v79
	v_pk_add_f32 v[78:79], v[48:49], v[88:89]
	v_pk_add_f32 v[48:49], v[48:49], v[88:89] neg_lo:[0,1] neg_hi:[0,1]
	v_pk_add_f32 v[88:89], v[76:77], v[78:79]
	v_xor_b32_e32 v86, 0x80000000, v49
	v_mov_b32_e32 v87, v48
	v_pk_mul_f32 v[86:87], v[10:11], v[86:87] op_sel_hi:[0,1] neg_lo:[1,0] neg_hi:[1,0]
	v_pk_fma_f32 v[48:49], v[10:11], v[48:49], v[86:87] op_sel_hi:[0,1,1] neg_lo:[1,0,0] neg_hi:[1,0,0]
	v_pk_add_f32 v[86:87], v[32:33], v[40:41]
	v_pk_add_f32 v[32:33], v[32:33], v[40:41] neg_lo:[0,1] neg_hi:[0,1]
	v_pk_add_f32 v[40:41], v[76:77], v[78:79] neg_lo:[0,1] neg_hi:[0,1]
	v_pk_add_f32 v[78:79], v[86:87], v[88:89] neg_lo:[0,1] neg_hi:[0,1]
	v_xor_b32_e32 v77, 0x80000000, v40
	v_mov_b32_e32 v76, v41
	v_pk_add_f32 v[90:91], v[32:33], v[76:77]
	v_pk_add_f32 v[40:41], v[32:33], v[76:77] neg_lo:[0,1] neg_hi:[0,1]
	v_pk_add_f32 v[76:77], v[54:55], v[48:49]
	v_pk_add_f32 v[48:49], v[54:55], v[48:49] neg_lo:[0,1] neg_hi:[0,1]
	v_pk_add_f32 v[32:33], v[60:61], v[82:83]
	v_pk_add_f32 v[60:61], v[60:61], v[82:83] neg_lo:[0,1] neg_hi:[0,1]
	v_xor_b32_e32 v55, 0x80000000, v48
	v_mov_b32_e32 v54, v49
	v_pk_add_f32 v[82:83], v[32:33], v[76:77]
	v_pk_add_f32 v[48:49], v[32:33], v[76:77] neg_lo:[0,1] neg_hi:[0,1]
	v_pk_add_f32 v[76:77], v[60:61], v[54:55]
	v_pk_add_f32 v[32:33], v[60:61], v[54:55] neg_lo:[0,1] neg_hi:[0,1]
	v_pk_add_f32 v[54:55], v[92:93], v[84:85]
	v_pk_add_f32 v[60:61], v[92:93], v[84:85] neg_lo:[0,1] neg_hi:[0,1]
	v_pk_add_f32 v[84:85], v[56:57], v[44:45]
	v_pk_add_f32 v[44:45], v[44:45], v[56:57] neg_lo:[0,1] neg_hi:[0,1]
	v_pk_add_f32 v[86:87], v[86:87], v[88:89]
	v_xor_b32_e32 v56, 0x80000000, v45
	v_mov_b32_e32 v57, v44
	v_pk_mul_f32 v[56:57], v[10:11], v[56:57] op_sel_hi:[0,1] neg_lo:[1,0] neg_hi:[1,0]
	v_pk_fma_f32 v[56:57], v[10:11], v[44:45], v[56:57] op_sel_hi:[0,1,1]
	v_pk_add_f32 v[44:45], v[80:81], v[58:59]
	v_pk_add_f32 v[58:59], v[80:81], v[58:59] neg_lo:[0,1] neg_hi:[0,1]
	v_xor_b32_e32 v88, 0x80000000, v87
	v_xor_b32_e32 v81, 0x80000000, v58
	v_mov_b32_e32 v80, v59
	v_pk_add_f32 v[58:59], v[52:53], v[36:37]
	v_pk_add_f32 v[36:37], v[52:53], v[36:37] neg_lo:[0,1] neg_hi:[0,1]
	v_mov_b32_e32 v89, v87
	v_xor_b32_e32 v52, 0x80000000, v37
	v_mov_b32_e32 v53, v36
	v_pk_mul_f32 v[52:53], v[10:11], v[52:53] op_sel_hi:[0,1] neg_lo:[1,0] neg_hi:[1,0]
	v_pk_fma_f32 v[36:37], v[10:11], v[36:37], v[52:53] op_sel_hi:[0,1,1] neg_lo:[1,0,0] neg_hi:[1,0,0]
	v_pk_add_f32 v[52:53], v[54:55], v[44:45]
	v_pk_add_f32 v[44:45], v[54:55], v[44:45] neg_lo:[0,1] neg_hi:[0,1]
	v_pk_add_f32 v[54:55], v[84:85], v[58:59]
	v_pk_add_f32 v[58:59], v[84:85], v[58:59] neg_lo:[0,1] neg_hi:[0,1]
	s_nop 0
	v_xor_b32_e32 v85, 0x80000000, v58
	v_mov_b32_e32 v84, v59
	v_pk_add_f32 v[58:59], v[52:53], v[54:55]
	v_pk_add_f32 v[52:53], v[52:53], v[54:55] neg_lo:[0,1] neg_hi:[0,1]
	v_pk_add_f32 v[54:55], v[44:45], v[84:85]
	v_pk_add_f32 v[44:45], v[44:45], v[84:85] neg_lo:[0,1] neg_hi:[0,1]
	v_pk_add_f32 v[84:85], v[60:61], v[80:81]
	v_pk_add_f32 v[60:61], v[60:61], v[80:81] neg_lo:[0,1] neg_hi:[0,1]
	v_pk_add_f32 v[80:81], v[56:57], v[36:37]
	v_pk_add_f32 v[36:37], v[56:57], v[36:37] neg_lo:[0,1] neg_hi:[0,1]
	v_pk_add_f32 v[92:93], v[84:85], v[80:81]
	v_xor_b32_e32 v57, 0x80000000, v36
	v_mov_b32_e32 v56, v37
	v_pk_add_f32 v[80:81], v[84:85], v[80:81] neg_lo:[0,1] neg_hi:[0,1]
	v_pk_add_f32 v[84:85], v[60:61], v[56:57]
	v_pk_add_f32 v[36:37], v[60:61], v[56:57] neg_lo:[0,1] neg_hi:[0,1]
	v_xor_b32_e32 v56, 0x80000000, v95
	v_mov_b32_e32 v57, v95
	v_pk_fma_f32 v[60:61], v[16:17], s[92:93], v[16:17] op_sel:[1,0,0] op_sel_hi:[0,1,1]
	v_pk_mul_f32 v[56:57], v[56:57], s[14:15]
	v_pk_mul_f32 v[88:89], v[60:61], v[88:89] op_sel:[1,0] op_sel_hi:[0,1]
	v_pk_fma_f32 v[56:57], v[94:95], s[42:43], v[56:57] op_sel_hi:[0,1,1]
	v_pk_fma_f32 v[86:87], v[60:61], v[86:87], v[88:89] op_sel_hi:[1,0,1]
	ds_write2_b64 v75, v[56:57], v[86:87] offset1:16
	v_xor_b32_e32 v56, 0x80000000, v61
	v_mov_b32_e32 v57, v61
	v_pk_mul_f32 v[56:57], v[16:17], v[56:57] op_sel:[1,0] op_sel_hi:[0,1]
	v_pk_fma_f32 v[56:57], v[16:17], v[60:61], v[56:57] op_sel_hi:[1,0,1]
	v_xor_b32_e32 v60, 0x80000000, v103
	v_mov_b32_e32 v61, v103
	v_xor_b32_e32 v86, 0x80000000, v57
	v_mov_b32_e32 v87, v57
	v_pk_mul_f32 v[60:61], v[56:57], v[60:61] op_sel:[1,0] op_sel_hi:[0,1]
	v_pk_mul_f32 v[86:87], v[16:17], v[86:87] op_sel:[1,0] op_sel_hi:[0,1]
	v_pk_fma_f32 v[60:61], v[56:57], v[102:103], v[60:61] op_sel_hi:[1,0,1]
	v_pk_fma_f32 v[56:57], v[16:17], v[56:57], v[86:87] op_sel_hi:[1,0,1]
	v_xor_b32_e32 v86, 0x80000000, v59
	v_mov_b32_e32 v87, v59
	v_pk_mul_f32 v[86:87], v[56:57], v[86:87] op_sel:[1,0] op_sel_hi:[0,1]
	v_pk_fma_f32 v[58:59], v[56:57], v[58:59], v[86:87] op_sel_hi:[1,0,1]
	ds_write2_b64 v74, v[60:61], v[58:59] offset0:32 offset1:48
	v_xor_b32_e32 v58, 0x80000000, v57
	v_mov_b32_e32 v59, v57
	v_pk_mul_f32 v[58:59], v[16:17], v[58:59] op_sel:[1,0] op_sel_hi:[0,1]
	v_pk_fma_f32 v[56:57], v[16:17], v[56:57], v[58:59] op_sel_hi:[1,0,1]
	v_xor_b32_e32 v58, 0x80000000, v105
	v_mov_b32_e32 v59, v105
	v_xor_b32_e32 v60, 0x80000000, v57
	v_mov_b32_e32 v61, v57
	v_pk_mul_f32 v[58:59], v[56:57], v[58:59] op_sel:[1,0] op_sel_hi:[0,1]
	v_pk_mul_f32 v[60:61], v[16:17], v[60:61] op_sel:[1,0] op_sel_hi:[0,1]
	v_pk_fma_f32 v[58:59], v[56:57], v[104:105], v[58:59] op_sel_hi:[1,0,1]
	v_pk_fma_f32 v[56:57], v[16:17], v[56:57], v[60:61] op_sel_hi:[1,0,1]
	v_xor_b32_e32 v60, 0x80000000, v83
	v_mov_b32_e32 v61, v83
	v_pk_mul_f32 v[60:61], v[56:57], v[60:61] op_sel:[1,0] op_sel_hi:[0,1]
	v_pk_fma_f32 v[60:61], v[56:57], v[82:83], v[60:61] op_sel_hi:[1,0,1]
	ds_write2_b64 v73, v[58:59], v[60:61] offset0:64 offset1:80
	v_xor_b32_e32 v58, 0x80000000, v57
	v_mov_b32_e32 v59, v57
	v_pk_mul_f32 v[58:59], v[16:17], v[58:59] op_sel:[1,0] op_sel_hi:[0,1]
	v_pk_fma_f32 v[56:57], v[16:17], v[56:57], v[58:59] op_sel_hi:[1,0,1]
	v_xor_b32_e32 v58, 0x80000000, v99
	v_mov_b32_e32 v59, v99
	v_xor_b32_e32 v60, 0x80000000, v57
	v_mov_b32_e32 v61, v57
	v_pk_mul_f32 v[58:59], v[56:57], v[58:59] op_sel:[1,0] op_sel_hi:[0,1]
	v_pk_mul_f32 v[60:61], v[16:17], v[60:61] op_sel:[1,0] op_sel_hi:[0,1]
	v_pk_fma_f32 v[58:59], v[56:57], v[98:99], v[58:59] op_sel_hi:[1,0,1]
	v_pk_fma_f32 v[56:57], v[16:17], v[56:57], v[60:61] op_sel_hi:[1,0,1]
	v_xor_b32_e32 v60, 0x80000000, v93
	v_mov_b32_e32 v61, v93
	v_pk_mul_f32 v[60:61], v[56:57], v[60:61] op_sel:[1,0] op_sel_hi:[0,1]
	v_pk_fma_f32 v[60:61], v[56:57], v[92:93], v[60:61] op_sel_hi:[1,0,1]
	ds_write2_b64 v72, v[58:59], v[60:61] offset0:96 offset1:112
	v_xor_b32_e32 v58, 0x80000000, v57
	v_mov_b32_e32 v59, v57
	v_pk_mul_f32 v[58:59], v[16:17], v[58:59] op_sel:[1,0] op_sel_hi:[0,1]
	v_pk_fma_f32 v[56:57], v[16:17], v[56:57], v[58:59] op_sel_hi:[1,0,1]
	v_xor_b32_e32 v58, 0x80000000, v47
	v_mov_b32_e32 v59, v47
	v_pk_mul_f32 v[58:59], v[56:57], v[58:59] op_sel:[1,0] op_sel_hi:[0,1]
	v_pk_fma_f32 v[46:47], v[56:57], v[46:47], v[58:59] op_sel_hi:[1,0,1]
	v_xor_b32_e32 v58, 0x80000000, v57
	v_mov_b32_e32 v59, v57
	v_pk_mul_f32 v[58:59], v[16:17], v[58:59] op_sel:[1,0] op_sel_hi:[0,1]
	v_pk_fma_f32 v[56:57], v[16:17], v[56:57], v[58:59] op_sel_hi:[1,0,1]
	v_xor_b32_e32 v58, 0x80000000, v91
	v_mov_b32_e32 v59, v91
	v_pk_mul_f32 v[58:59], v[56:57], v[58:59] op_sel:[1,0] op_sel_hi:[0,1]
	v_pk_fma_f32 v[58:59], v[56:57], v[90:91], v[58:59] op_sel_hi:[1,0,1]
	ds_write2_b64 v71, v[46:47], v[58:59] offset0:128 offset1:144
	v_xor_b32_e32 v46, 0x80000000, v57
	v_mov_b32_e32 v47, v57
	v_pk_mul_f32 v[46:47], v[16:17], v[46:47] op_sel:[1,0] op_sel_hi:[0,1]
	v_pk_fma_f32 v[46:47], v[16:17], v[56:57], v[46:47] op_sel_hi:[1,0,1]
	v_xor_b32_e32 v56, 0x80000000, v51
	v_mov_b32_e32 v57, v51
	v_pk_mul_f32 v[56:57], v[46:47], v[56:57] op_sel:[1,0] op_sel_hi:[0,1]
	v_pk_fma_f32 v[50:51], v[46:47], v[50:51], v[56:57] op_sel_hi:[1,0,1]
	v_xor_b32_e32 v56, 0x80000000, v47
	v_mov_b32_e32 v57, v47
	v_pk_mul_f32 v[56:57], v[16:17], v[56:57] op_sel:[1,0] op_sel_hi:[0,1]
	v_pk_fma_f32 v[46:47], v[16:17], v[46:47], v[56:57] op_sel_hi:[1,0,1]
	v_xor_b32_e32 v56, 0x80000000, v55
	v_mov_b32_e32 v57, v55
	v_pk_mul_f32 v[56:57], v[46:47], v[56:57] op_sel:[1,0] op_sel_hi:[0,1]
	v_pk_fma_f32 v[54:55], v[46:47], v[54:55], v[56:57] op_sel_hi:[1,0,1]
	ds_write2_b64 v70, v[50:51], v[54:55] offset0:160 offset1:176
	v_xor_b32_e32 v50, 0x80000000, v47
	v_mov_b32_e32 v51, v47
	v_pk_mul_f32 v[50:51], v[16:17], v[50:51] op_sel:[1,0] op_sel_hi:[0,1]
	v_pk_fma_f32 v[46:47], v[16:17], v[46:47], v[50:51] op_sel_hi:[1,0,1]
	v_xor_b32_e32 v50, 0x80000000, v39
	v_mov_b32_e32 v51, v39
	v_pk_mul_f32 v[50:51], v[50:51], v[46:47] op_sel:[0,1] op_sel_hi:[1,0]
	s_nop 0
	v_pk_fma_f32 v[38:39], v[38:39], v[46:47], v[50:51] op_sel_hi:[0,1,1]
	v_xor_b32_e32 v50, 0x80000000, v47
	v_mov_b32_e32 v51, v47
	v_pk_mul_f32 v[50:51], v[16:17], v[50:51] op_sel:[1,0] op_sel_hi:[0,1]
	v_pk_fma_f32 v[46:47], v[16:17], v[46:47], v[50:51] op_sel_hi:[1,0,1]
	v_xor_b32_e32 v50, 0x80000000, v77
	v_mov_b32_e32 v51, v77
	v_pk_mul_f32 v[50:51], v[46:47], v[50:51] op_sel:[1,0] op_sel_hi:[0,1]
	v_pk_fma_f32 v[50:51], v[46:47], v[76:77], v[50:51] op_sel_hi:[1,0,1]
	ds_write2_b64 v69, v[38:39], v[50:51] offset0:192 offset1:208
	v_xor_b32_e32 v38, 0x80000000, v47
	v_mov_b32_e32 v39, v47
	v_pk_mul_f32 v[38:39], v[16:17], v[38:39] op_sel:[1,0] op_sel_hi:[0,1]
	v_pk_fma_f32 v[38:39], v[16:17], v[46:47], v[38:39] op_sel_hi:[1,0,1]
	v_xor_b32_e32 v46, 0x80000000, v43
	v_mov_b32_e32 v47, v43
	v_pk_mul_f32 v[46:47], v[46:47], v[38:39] op_sel:[0,1] op_sel_hi:[1,0]
	s_nop 0
	v_pk_fma_f32 v[42:43], v[42:43], v[38:39], v[46:47] op_sel_hi:[0,1,1]
	v_xor_b32_e32 v46, 0x80000000, v39
	v_mov_b32_e32 v47, v39
	v_pk_mul_f32 v[46:47], v[16:17], v[46:47] op_sel:[1,0] op_sel_hi:[0,1]
	v_pk_fma_f32 v[38:39], v[16:17], v[38:39], v[46:47] op_sel_hi:[1,0,1]
	v_xor_b32_e32 v46, 0x80000000, v85
	v_mov_b32_e32 v47, v85
	v_pk_mul_f32 v[46:47], v[38:39], v[46:47] op_sel:[1,0] op_sel_hi:[0,1]
	v_pk_fma_f32 v[46:47], v[38:39], v[84:85], v[46:47] op_sel_hi:[1,0,1]
	ds_write2_b64 v68, v[42:43], v[46:47] offset0:224 offset1:240
	v_xor_b32_e32 v42, 0x80000000, v39
	v_mov_b32_e32 v43, v39
	v_pk_mul_f32 v[42:43], v[16:17], v[42:43] op_sel:[1,0] op_sel_hi:[0,1]
	v_pk_fma_f32 v[38:39], v[16:17], v[38:39], v[42:43] op_sel_hi:[1,0,1]
	v_xor_b32_e32 v42, 0x80000000, v31
	v_mov_b32_e32 v43, v31
	v_pk_mul_f32 v[42:43], v[42:43], v[38:39] op_sel:[0,1] op_sel_hi:[1,0]
	s_nop 0
	v_pk_fma_f32 v[30:31], v[30:31], v[38:39], v[42:43] op_sel_hi:[0,1,1]
	v_xor_b32_e32 v42, 0x80000000, v39
	v_mov_b32_e32 v43, v39
	v_pk_mul_f32 v[42:43], v[16:17], v[42:43] op_sel:[1,0] op_sel_hi:[0,1]
	v_pk_fma_f32 v[38:39], v[16:17], v[38:39], v[42:43] op_sel_hi:[1,0,1]
	v_xor_b32_e32 v42, 0x80000000, v79
	v_mov_b32_e32 v43, v79
	v_pk_mul_f32 v[42:43], v[42:43], v[38:39] op_sel:[0,1] op_sel_hi:[1,0]
	s_nop 0
	v_pk_fma_f32 v[42:43], v[78:79], v[38:39], v[42:43] op_sel_hi:[0,1,1]
	ds_write2_b64 v67, v[30:31], v[42:43] offset1:16
	v_xor_b32_e32 v30, 0x80000000, v39
	v_mov_b32_e32 v31, v39
	v_pk_mul_f32 v[30:31], v[16:17], v[30:31] op_sel:[1,0] op_sel_hi:[0,1]
	v_pk_fma_f32 v[30:31], v[16:17], v[38:39], v[30:31] op_sel_hi:[1,0,1]
	v_xor_b32_e32 v38, 0x80000000, v35
	v_mov_b32_e32 v39, v35
	v_pk_mul_f32 v[38:39], v[38:39], v[30:31] op_sel:[0,1] op_sel_hi:[1,0]
	s_nop 0
	v_pk_fma_f32 v[34:35], v[34:35], v[30:31], v[38:39] op_sel_hi:[0,1,1]
	v_xor_b32_e32 v38, 0x80000000, v31
	v_mov_b32_e32 v39, v31
	v_pk_mul_f32 v[38:39], v[16:17], v[38:39] op_sel:[1,0] op_sel_hi:[0,1]
	v_pk_fma_f32 v[30:31], v[16:17], v[30:31], v[38:39] op_sel_hi:[1,0,1]
	v_xor_b32_e32 v38, 0x80000000, v53
	v_mov_b32_e32 v39, v53
	v_pk_mul_f32 v[38:39], v[38:39], v[30:31] op_sel:[0,1] op_sel_hi:[1,0]
	s_nop 0
	v_pk_fma_f32 v[38:39], v[52:53], v[30:31], v[38:39] op_sel_hi:[0,1,1]
	ds_write2_b64 v66, v[34:35], v[38:39] offset0:32 offset1:48
	v_xor_b32_e32 v34, 0x80000000, v31
	v_mov_b32_e32 v35, v31
	v_pk_mul_f32 v[34:35], v[16:17], v[34:35] op_sel:[1,0] op_sel_hi:[0,1]
	v_pk_fma_f32 v[30:31], v[16:17], v[30:31], v[34:35] op_sel_hi:[1,0,1]
	v_xor_b32_e32 v34, 0x80000000, v27
	v_mov_b32_e32 v35, v27
	v_pk_mul_f32 v[34:35], v[34:35], v[30:31] op_sel:[0,1] op_sel_hi:[1,0]
	s_nop 0
	v_pk_fma_f32 v[26:27], v[26:27], v[30:31], v[34:35] op_sel_hi:[0,1,1]
	v_xor_b32_e32 v34, 0x80000000, v31
	v_mov_b32_e32 v35, v31
	v_pk_mul_f32 v[34:35], v[16:17], v[34:35] op_sel:[1,0] op_sel_hi:[0,1]
	v_pk_fma_f32 v[30:31], v[16:17], v[30:31], v[34:35] op_sel_hi:[1,0,1]
	v_xor_b32_e32 v34, 0x80000000, v49
	v_mov_b32_e32 v35, v49
	v_pk_mul_f32 v[34:35], v[34:35], v[30:31] op_sel:[0,1] op_sel_hi:[1,0]
	s_nop 0
	v_pk_fma_f32 v[34:35], v[48:49], v[30:31], v[34:35] op_sel_hi:[0,1,1]
	ds_write2_b64 v65, v[26:27], v[34:35] offset0:64 offset1:80
	v_xor_b32_e32 v26, 0x80000000, v31
	v_mov_b32_e32 v27, v31
	v_pk_mul_f32 v[26:27], v[16:17], v[26:27] op_sel:[1,0] op_sel_hi:[0,1]
	v_pk_fma_f32 v[26:27], v[16:17], v[30:31], v[26:27] op_sel_hi:[1,0,1]
	v_xor_b32_e32 v30, 0x80000000, v29
	v_mov_b32_e32 v31, v29
	v_pk_mul_f32 v[30:31], v[30:31], v[26:27] op_sel:[0,1] op_sel_hi:[1,0]
	s_nop 0
	v_pk_fma_f32 v[28:29], v[28:29], v[26:27], v[30:31] op_sel_hi:[0,1,1]
	v_xor_b32_e32 v30, 0x80000000, v27
	v_mov_b32_e32 v31, v27
	v_pk_mul_f32 v[30:31], v[16:17], v[30:31] op_sel:[1,0] op_sel_hi:[0,1]
	v_pk_fma_f32 v[26:27], v[16:17], v[26:27], v[30:31] op_sel_hi:[1,0,1]
	v_xor_b32_e32 v30, 0x80000000, v81
	v_mov_b32_e32 v31, v81
	v_pk_mul_f32 v[30:31], v[30:31], v[26:27] op_sel:[0,1] op_sel_hi:[1,0]
	s_nop 0
	v_pk_fma_f32 v[30:31], v[80:81], v[26:27], v[30:31] op_sel_hi:[0,1,1]
	ds_write2_b64 v64, v[28:29], v[30:31] offset0:96 offset1:112
	v_xor_b32_e32 v28, 0x80000000, v27
	v_mov_b32_e32 v29, v27
	v_pk_mul_f32 v[28:29], v[16:17], v[28:29] op_sel:[1,0] op_sel_hi:[0,1]
	v_pk_fma_f32 v[26:27], v[16:17], v[26:27], v[28:29] op_sel_hi:[1,0,1]
	v_xor_b32_e32 v28, 0x80000000, v23
	v_mov_b32_e32 v29, v23
	v_pk_mul_f32 v[28:29], v[28:29], v[26:27] op_sel:[0,1] op_sel_hi:[1,0]
	s_nop 0
	v_pk_fma_f32 v[22:23], v[22:23], v[26:27], v[28:29] op_sel_hi:[0,1,1]
	v_xor_b32_e32 v28, 0x80000000, v27
	v_mov_b32_e32 v29, v27
	v_pk_mul_f32 v[28:29], v[16:17], v[28:29] op_sel:[1,0] op_sel_hi:[0,1]
	v_pk_fma_f32 v[26:27], v[16:17], v[26:27], v[28:29] op_sel_hi:[1,0,1]
	v_xor_b32_e32 v28, 0x80000000, v41
	v_mov_b32_e32 v29, v41
	v_pk_mul_f32 v[28:29], v[28:29], v[26:27] op_sel:[0,1] op_sel_hi:[1,0]
	s_nop 0
	v_pk_fma_f32 v[28:29], v[40:41], v[26:27], v[28:29] op_sel_hi:[0,1,1]
	ds_write2_b64 v63, v[22:23], v[28:29] offset0:128 offset1:144
	v_xor_b32_e32 v22, 0x80000000, v27
	v_mov_b32_e32 v23, v27
	v_pk_mul_f32 v[22:23], v[16:17], v[22:23] op_sel:[1,0] op_sel_hi:[0,1]
	v_pk_fma_f32 v[22:23], v[16:17], v[26:27], v[22:23] op_sel_hi:[1,0,1]
	v_xor_b32_e32 v26, 0x80000000, v25
	v_mov_b32_e32 v27, v25
	v_pk_mul_f32 v[26:27], v[26:27], v[22:23] op_sel:[0,1] op_sel_hi:[1,0]
	s_nop 0
	v_pk_fma_f32 v[24:25], v[24:25], v[22:23], v[26:27] op_sel_hi:[0,1,1]
	v_xor_b32_e32 v26, 0x80000000, v23
	v_mov_b32_e32 v27, v23
	v_pk_mul_f32 v[26:27], v[16:17], v[26:27] op_sel:[1,0] op_sel_hi:[0,1]
	v_pk_fma_f32 v[22:23], v[16:17], v[22:23], v[26:27] op_sel_hi:[1,0,1]
	v_xor_b32_e32 v26, 0x80000000, v45
	v_mov_b32_e32 v27, v45
	v_pk_mul_f32 v[26:27], v[26:27], v[22:23] op_sel:[0,1] op_sel_hi:[1,0]
	s_nop 0
	v_pk_fma_f32 v[26:27], v[44:45], v[22:23], v[26:27] op_sel_hi:[0,1,1]
	ds_write2_b64 v62, v[24:25], v[26:27] offset0:160 offset1:176
	v_xor_b32_e32 v24, 0x80000000, v23
	v_mov_b32_e32 v25, v23
	v_pk_mul_f32 v[24:25], v[16:17], v[24:25] op_sel:[1,0] op_sel_hi:[0,1]
	v_pk_fma_f32 v[22:23], v[16:17], v[22:23], v[24:25] op_sel_hi:[1,0,1]
	v_xor_b32_e32 v24, 0x80000000, v19
	v_mov_b32_e32 v25, v19
	v_pk_mul_f32 v[24:25], v[24:25], v[22:23] op_sel:[0,1] op_sel_hi:[1,0]
	s_nop 0
	v_pk_fma_f32 v[18:19], v[18:19], v[22:23], v[24:25] op_sel_hi:[0,1,1]
	v_xor_b32_e32 v24, 0x80000000, v23
	v_mov_b32_e32 v25, v23
	v_pk_mul_f32 v[24:25], v[16:17], v[24:25] op_sel:[1,0] op_sel_hi:[0,1]
	v_pk_fma_f32 v[22:23], v[16:17], v[22:23], v[24:25] op_sel_hi:[1,0,1]
	v_xor_b32_e32 v24, 0x80000000, v33
	v_mov_b32_e32 v25, v33
	v_pk_mul_f32 v[24:25], v[24:25], v[22:23] op_sel:[0,1] op_sel_hi:[1,0]
	s_nop 0
	v_pk_fma_f32 v[24:25], v[32:33], v[22:23], v[24:25] op_sel_hi:[0,1,1]
	ds_write2_b64 v15, v[18:19], v[24:25] offset0:192 offset1:208
	v_xor_b32_e32 v18, 0x80000000, v23
	v_mov_b32_e32 v19, v23
	v_pk_mul_f32 v[18:19], v[16:17], v[18:19] op_sel:[1,0] op_sel_hi:[0,1]
	v_pk_fma_f32 v[18:19], v[16:17], v[22:23], v[18:19] op_sel_hi:[1,0,1]
	v_xor_b32_e32 v22, 0x80000000, v21
	v_mov_b32_e32 v23, v21
	v_pk_mul_f32 v[22:23], v[22:23], v[18:19] op_sel:[0,1] op_sel_hi:[1,0]
	s_nop 0
	v_pk_fma_f32 v[20:21], v[20:21], v[18:19], v[22:23] op_sel_hi:[0,1,1]
	v_xor_b32_e32 v22, 0x80000000, v19
	v_mov_b32_e32 v23, v19
	v_pk_mul_f32 v[22:23], v[16:17], v[22:23] op_sel:[1,0] op_sel_hi:[0,1]
	v_pk_fma_f32 v[16:17], v[16:17], v[18:19], v[22:23] op_sel_hi:[1,0,1]
	v_xor_b32_e32 v18, 0x80000000, v37
	v_mov_b32_e32 v19, v37
	v_pk_mul_f32 v[18:19], v[18:19], v[16:17] op_sel:[0,1] op_sel_hi:[1,0]
	s_nop 0
	v_pk_fma_f32 v[16:17], v[36:37], v[16:17], v[18:19] op_sel_hi:[0,1,1]
	ds_write2_b64 v13, v[20:21], v[16:17] offset0:224 offset1:240
	v_mov_b32_e32 v16, v1
	v_mov_b32_e32 v10, v178
	v_mov_b32_e32 v17, v177
	s_waitcnt lgkmcnt(0)
	s_barrier
	v_lshlrev_b32_e32 v190, 3, v16
	v_add_u32_e32 v190, 0x1000, v190
	global_load_dwordx2 v[196:197], v190, s[48:49] offset:-4096
	global_load_dwordx2 v[198:199], v190, s[48:49]
	v_add_u32_e32 v190, 0x2000, v190
	global_load_dwordx2 v[200:201], v190, s[48:49] offset:-4096
	global_load_dwordx2 v[202:203], v190, s[48:49]
	v_add_u32_e32 v190, 0x2000, v190
	global_load_dwordx2 v[204:205], v190, s[48:49] offset:-4096
	global_load_dwordx2 v[206:207], v190, s[48:49]
	v_add_u32_e32 v190, 0x2000, v190
	global_load_dwordx2 v[208:209], v190, s[48:49] offset:-4096
	global_load_dwordx2 v[210:211], v190, s[48:49]
	v_add_u32_e32 v190, 0x2000, v190
	global_load_dwordx2 v[212:213], v190, s[48:49] offset:-4096
	global_load_dwordx2 v[214:215], v190, s[48:49]
	v_add_u32_e32 v190, 0x2000, v190
	global_load_dwordx2 v[216:217], v190, s[48:49] offset:-4096
	global_load_dwordx2 v[218:219], v190, s[48:49]
	v_add_u32_e32 v190, 0x2000, v190
	global_load_dwordx2 v[220:221], v190, s[48:49] offset:-4096
	global_load_dwordx2 v[222:223], v190, s[48:49]
	v_add_u32_e32 v190, 0x2000, v190
	global_load_dwordx2 v[224:225], v190, s[48:49] offset:-4096
	global_load_dwordx2 v[226:227], v190, s[48:49]
	v_mov_b32_e32 v50, v166
	v_lshlrev_b32_e32 v13, 3, v17
	v_lshlrev_b32_e32 v48, 3, v10
	v_add3_u32 v10, 0, v13, v48
	v_xor_b32_e32 v13, 1, v17
	v_xor_b32_e32 v34, 8, v17
	v_xor_b32_e32 v36, 9, v17
	v_lshlrev_b32_e32 v13, 3, v13
	v_xor_b32_e32 v15, 2, v17
	v_xor_b32_e32 v24, 3, v17
	v_xor_b32_e32 v26, 4, v17
	v_xor_b32_e32 v28, 5, v17
	v_xor_b32_e32 v30, 6, v17
	v_xor_b32_e32 v32, 7, v17
	v_lshlrev_b32_e32 v34, 3, v34
	v_lshlrev_b32_e32 v36, 3, v36
	v_xor_b32_e32 v38, 10, v17
	v_xor_b32_e32 v40, 11, v17
	v_xor_b32_e32 v42, 12, v17
	v_xor_b32_e32 v44, 13, v17
	v_xor_b32_e32 v46, 14, v17
	v_xor_b32_e32 v17, 15, v17
	v_add3_u32 v13, 0, v13, v48
	v_lshlrev_b32_e32 v15, 3, v15
	v_lshlrev_b32_e32 v24, 3, v24
	v_lshlrev_b32_e32 v26, 3, v26
	v_lshlrev_b32_e32 v28, 3, v28
	v_lshlrev_b32_e32 v30, 3, v30
	v_lshlrev_b32_e32 v32, 3, v32
	v_add3_u32 v57, 0, v34, v48
	v_add3_u32 v58, 0, v36, v48
	v_lshlrev_b32_e32 v38, 3, v38
	v_lshlrev_b32_e32 v40, 3, v40
	v_lshlrev_b32_e32 v42, 3, v42
	v_lshlrev_b32_e32 v44, 3, v44
	v_lshlrev_b32_e32 v46, 3, v46
	v_lshlrev_b32_e32 v17, 3, v17
	ds_read_b64 v[18:19], v10
	ds_read_b64 v[20:21], v13
	v_add3_u32 v15, 0, v15, v48
	v_add3_u32 v52, 0, v24, v48
	v_add3_u32 v53, 0, v26, v48
	v_add3_u32 v54, 0, v28, v48
	v_add3_u32 v55, 0, v30, v48
	v_add3_u32 v56, 0, v32, v48
	ds_read_b64 v[34:35], v57
	ds_read_b64 v[36:37], v58
	v_add3_u32 v59, 0, v38, v48
	v_add3_u32 v60, 0, v40, v48
	v_add3_u32 v61, 0, v42, v48
	v_add3_u32 v62, 0, v44, v48
	v_add3_u32 v63, 0, v46, v48
	v_add3_u32 v64, 0, v17, v48
	v_mov_b32_e32 v17, v164
	ds_read_b64 v[22:23], v15
	ds_read_b64 v[24:25], v52
	ds_read_b64 v[26:27], v53
	ds_read_b64 v[28:29], v54
	ds_read_b64 v[30:31], v55
	ds_read_b64 v[32:33], v56
	ds_read_b64 v[38:39], v59
	ds_read_b64 v[40:41], v60
	ds_read_b64 v[42:43], v61
	ds_read_b64 v[44:45], v62
	ds_read_b64 v[46:47], v63
	ds_read_b64 v[48:49], v64
	s_waitcnt lgkmcnt(13)
	v_pk_add_f32 v[70:71], v[18:19], v[34:35]
	v_mov_b32_e32 v17, v165
	v_pk_add_f32 v[18:19], v[18:19], v[34:35] neg_lo:[0,1] neg_hi:[0,1]
	v_mov_b32_e32 v17, v167
	s_waitcnt lgkmcnt(12)
	v_pk_add_f32 v[34:35], v[20:21], v[36:37]
	v_pk_add_f32 v[20:21], v[20:21], v[36:37] neg_lo:[0,1] neg_hi:[0,1]
	v_mov_b32_e32 v66, v168
	v_mov_b32_e32 v17, v169
	v_mov_b32_e32 v68, v170
	v_xor_b32_e32 v36, 0x80000000, v21
	v_mov_b32_e32 v37, v20
	s_nop 0
	v_pk_mul_f32 v[36:37], v[36:37], v[68:69] op_sel_hi:[1,0] neg_lo:[0,1] neg_hi:[0,1]
	v_mov_b32_e32 v17, v171
	v_pk_fma_f32 v[20:21], v[20:21], v[50:51], v[36:37] op_sel_hi:[1,0,1]
	s_waitcnt lgkmcnt(5)
	v_pk_add_f32 v[36:37], v[22:23], v[38:39]
	v_pk_add_f32 v[22:23], v[22:23], v[38:39] neg_lo:[0,1] neg_hi:[0,1]
	s_nop 0
	v_xor_b32_e32 v38, 0x80000000, v23
	v_mov_b32_e32 v39, v22
	v_pk_mul_f32 v[38:39], v[38:39], v[66:67] op_sel_hi:[1,0] neg_lo:[0,1] neg_hi:[0,1]
	v_mov_b32_e32 v17, v172
	v_pk_fma_f32 v[22:23], v[22:23], v[66:67], v[38:39] op_sel_hi:[1,0,1]
	s_waitcnt lgkmcnt(4)
	v_pk_add_f32 v[38:39], v[24:25], v[40:41]
	v_pk_add_f32 v[24:25], v[24:25], v[40:41] neg_lo:[0,1] neg_hi:[0,1]
	s_nop 0
	v_pk_mul_f32 v[40:41], v[24:25], v[68:69] op_sel_hi:[1,0]
	v_xor_b32_e32 v72, 0x80000000, v25
	v_mov_b32_e32 v73, v24
	v_pk_fma_f32 v[24:25], v[72:73], v[50:51], v[40:41] op_sel_hi:[1,0,1] neg_lo:[0,1,0] neg_hi:[0,1,0]
	s_waitcnt lgkmcnt(3)
	v_pk_add_f32 v[40:41], v[26:27], v[42:43]
	v_pk_add_f32 v[26:27], v[26:27], v[42:43] neg_lo:[0,1] neg_hi:[0,1]
	v_ashrrev_i32_e32 v17, 31, v16
	v_xor_b32_e32 v73, 0x80000000, v26
	v_mov_b32_e32 v72, v27
	s_waitcnt lgkmcnt(2)
	v_pk_add_f32 v[26:27], v[28:29], v[44:45]
	v_pk_add_f32 v[28:29], v[28:29], v[44:45] neg_lo:[0,1] neg_hi:[0,1]
	s_nop 0
	v_pk_mul_f32 v[42:43], v[28:29], v[68:69] op_sel_hi:[1,0] neg_lo:[0,1] neg_hi:[0,1]
	v_xor_b32_e32 v44, 0x80000000, v29
	v_mov_b32_e32 v45, v28
	v_pk_fma_f32 v[28:29], v[44:45], v[50:51], v[42:43] op_sel_hi:[1,0,1] neg_lo:[0,1,0] neg_hi:[0,1,0]
	s_waitcnt lgkmcnt(1)
	v_pk_add_f32 v[42:43], v[30:31], v[46:47]
	v_pk_add_f32 v[30:31], v[30:31], v[46:47] neg_lo:[0,1] neg_hi:[0,1]
	s_nop 0
	v_xor_b32_e32 v44, 0x80000000, v31
	v_mov_b32_e32 v45, v30
	v_pk_mul_f32 v[44:45], v[44:45], v[66:67] op_sel_hi:[1,0] neg_lo:[0,1] neg_hi:[0,1]
	s_nop 0
	v_pk_fma_f32 v[30:31], v[30:31], v[66:67], v[44:45] op_sel_hi:[1,0,1] neg_lo:[0,1,0] neg_hi:[0,1,0]
	s_waitcnt lgkmcnt(0)
	v_pk_add_f32 v[44:45], v[32:33], v[48:49]
	v_pk_add_f32 v[32:33], v[32:33], v[48:49] neg_lo:[0,1] neg_hi:[0,1]
	v_pk_add_f32 v[48:49], v[34:35], v[26:27]
	v_pk_add_f32 v[26:27], v[34:35], v[26:27] neg_lo:[0,1] neg_hi:[0,1]
	v_xor_b32_e32 v46, 0x80000000, v33
	v_xor_b32_e32 v34, 0x80000000, v27
	v_mov_b32_e32 v35, v26
	v_pk_mul_f32 v[34:35], v[34:35], v[66:67] op_sel_hi:[1,0] neg_lo:[0,1] neg_hi:[0,1]
	v_mov_b32_e32 v47, v32
	v_pk_fma_f32 v[26:27], v[26:27], v[66:67], v[34:35] op_sel_hi:[1,0,1]
	v_pk_add_f32 v[34:35], v[36:37], v[42:43]
	v_pk_add_f32 v[36:37], v[36:37], v[42:43] neg_lo:[0,1] neg_hi:[0,1]
	v_pk_mul_f32 v[46:47], v[46:47], v[68:69] op_sel_hi:[1,0] neg_lo:[0,1] neg_hi:[0,1]
	v_xor_b32_e32 v43, 0x80000000, v36
	v_mov_b32_e32 v42, v37
	v_pk_add_f32 v[36:37], v[38:39], v[44:45]
	v_pk_add_f32 v[38:39], v[38:39], v[44:45] neg_lo:[0,1] neg_hi:[0,1]
	v_pk_fma_f32 v[46:47], v[32:33], v[50:51], v[46:47] op_sel_hi:[1,0,1] neg_lo:[0,1,0] neg_hi:[0,1,0]
	v_xor_b32_e32 v44, 0x80000000, v39
	v_mov_b32_e32 v45, v38
	v_pk_add_f32 v[32:33], v[70:71], v[40:41]
	v_pk_mul_f32 v[44:45], v[44:45], v[66:67] op_sel_hi:[1,0] neg_lo:[0,1] neg_hi:[0,1]
	v_pk_add_f32 v[40:41], v[70:71], v[40:41] neg_lo:[0,1] neg_hi:[0,1]
	v_pk_fma_f32 v[38:39], v[38:39], v[66:67], v[44:45] op_sel_hi:[1,0,1] neg_lo:[0,1,0] neg_hi:[0,1,0]
	v_pk_add_f32 v[44:45], v[32:33], v[34:35]
	v_pk_add_f32 v[32:33], v[32:33], v[34:35] neg_lo:[0,1] neg_hi:[0,1]
	v_pk_add_f32 v[34:35], v[48:49], v[36:37]
	v_pk_add_f32 v[36:37], v[48:49], v[36:37] neg_lo:[0,1] neg_hi:[0,1]
	v_pk_add_f32 v[50:51], v[44:45], v[34:35]
	v_xor_b32_e32 v49, 0x80000000, v36
	v_mov_b32_e32 v48, v37
	v_pk_add_f32 v[36:37], v[44:45], v[34:35] neg_lo:[0,1] neg_hi:[0,1]
	v_pk_add_f32 v[68:69], v[32:33], v[48:49]
	v_pk_add_f32 v[44:45], v[32:33], v[48:49] neg_lo:[0,1] neg_hi:[0,1]
	v_pk_add_f32 v[32:33], v[40:41], v[42:43]
	v_pk_add_f32 v[34:35], v[40:41], v[42:43] neg_lo:[0,1] neg_hi:[0,1]
	v_pk_add_f32 v[40:41], v[26:27], v[38:39]
	v_pk_add_f32 v[26:27], v[26:27], v[38:39] neg_lo:[0,1] neg_hi:[0,1]
	v_pk_add_f32 v[42:43], v[32:33], v[40:41] neg_lo:[0,1] neg_hi:[0,1]
	v_xor_b32_e32 v39, 0x80000000, v26
	v_mov_b32_e32 v38, v27
	v_pk_add_f32 v[26:27], v[32:33], v[40:41]
	v_pk_add_f32 v[40:41], v[20:21], v[28:29]
	v_pk_add_f32 v[20:21], v[20:21], v[28:29] neg_lo:[0,1] neg_hi:[0,1]
	v_pk_add_f32 v[32:33], v[34:35], v[38:39]
	v_xor_b32_e32 v28, 0x80000000, v21
	v_mov_b32_e32 v29, v20
	v_pk_mul_f32 v[28:29], v[66:67], v[28:29] op_sel_hi:[0,1] neg_lo:[1,0] neg_hi:[1,0]
	v_pk_fma_f32 v[20:21], v[66:67], v[20:21], v[28:29] op_sel_hi:[0,1,1]
	v_pk_add_f32 v[28:29], v[22:23], v[30:31]
	v_pk_add_f32 v[22:23], v[22:23], v[30:31] neg_lo:[0,1] neg_hi:[0,1]
	v_pk_add_f32 v[38:39], v[34:35], v[38:39] neg_lo:[0,1] neg_hi:[0,1]
	v_xor_b32_e32 v31, 0x80000000, v22
	v_mov_b32_e32 v30, v23
	v_pk_add_f32 v[22:23], v[24:25], v[46:47]
	v_pk_add_f32 v[24:25], v[24:25], v[46:47] neg_lo:[0,1] neg_hi:[0,1]
	v_pk_add_f32 v[34:35], v[18:19], v[72:73]
	v_xor_b32_e32 v46, 0x80000000, v25
	v_mov_b32_e32 v47, v24
	v_pk_mul_f32 v[46:47], v[66:67], v[46:47] op_sel_hi:[0,1] neg_lo:[1,0] neg_hi:[1,0]
	v_pk_fma_f32 v[24:25], v[66:67], v[24:25], v[46:47] op_sel_hi:[0,1,1] neg_lo:[1,0,0] neg_hi:[1,0,0]
	v_pk_add_f32 v[46:47], v[34:35], v[28:29]
	v_pk_add_f32 v[28:29], v[34:35], v[28:29] neg_lo:[0,1] neg_hi:[0,1]
	v_pk_add_f32 v[34:35], v[40:41], v[22:23]
	v_pk_add_f32 v[22:23], v[40:41], v[22:23] neg_lo:[0,1] neg_hi:[0,1]
	v_pk_add_f32 v[18:19], v[18:19], v[72:73] neg_lo:[0,1] neg_hi:[0,1]
	v_xor_b32_e32 v49, 0x80000000, v22
	v_mov_b32_e32 v48, v23
	v_pk_add_f32 v[66:67], v[28:29], v[48:49]
	v_pk_add_f32 v[48:49], v[28:29], v[48:49] neg_lo:[0,1] neg_hi:[0,1]
	v_pk_add_f32 v[28:29], v[18:19], v[30:31]
	v_pk_add_f32 v[18:19], v[18:19], v[30:31] neg_lo:[0,1] neg_hi:[0,1]
	v_pk_add_f32 v[30:31], v[20:21], v[24:25]
	v_pk_add_f32 v[20:21], v[20:21], v[24:25] neg_lo:[0,1] neg_hi:[0,1]
	v_pk_add_f32 v[22:23], v[46:47], v[34:35]
	v_xor_b32_e32 v25, 0x80000000, v20
	v_mov_b32_e32 v24, v21
	v_lshl_add_u64 v[20:21], v[16:17], 3, s[48:49]
	s_waitcnt vmcnt(0)
	v_mov_b32_e32 v20, v196
	v_mov_b32_e32 v21, v197
	v_pk_add_f32 v[40:41], v[46:47], v[34:35] neg_lo:[0,1] neg_hi:[0,1]
	v_pk_add_f32 v[34:35], v[18:19], v[24:25]
	v_pk_add_f32 v[18:19], v[18:19], v[24:25] neg_lo:[0,1] neg_hi:[0,1]
	v_xor_b32_e32 v24, 0x80000000, v51
	v_mov_b32_e32 v25, v51
	v_pk_add_f32 v[70:71], v[28:29], v[30:31]
	v_pk_add_f32 v[46:47], v[28:29], v[30:31] neg_lo:[0,1] neg_hi:[0,1]
	v_xor_b32_e32 v28, 0x80000000, v23
	v_mov_b32_e32 v29, v23
	v_xor_b32_e32 v30, 0x80000000, v69
	v_mov_b32_e32 v31, v69
	v_mov_b32_e32 v17, v164
	s_nop 0
	v_pk_mul_f32 v[24:25], v[24:25], v[20:21] op_sel:[0,1] op_sel_hi:[1,0]
	s_nop 0
	v_pk_fma_f32 v[20:21], v[50:51], v[20:21], v[24:25] op_sel_hi:[0,1,1]
	v_add_u32_e32 v24, 0x200, v16
	v_ashrrev_i32_e32 v25, 31, v24
	v_lshl_add_u64 v[24:25], v[24:25], 3, s[48:49]
	v_mov_b32_e32 v24, v198
	v_mov_b32_e32 v25, v199
	v_xor_b32_e32 v50, 0x80000000, v67
	v_mov_b32_e32 v51, v67
	s_nop 0
	v_pk_mul_f32 v[28:29], v[24:25], v[28:29] op_sel:[1,0] op_sel_hi:[0,1]
	v_pk_fma_f32 v[22:23], v[24:25], v[22:23], v[28:29] op_sel_hi:[1,0,1]
	v_add_u32_e32 v24, 0x400, v16
	v_ashrrev_i32_e32 v25, 31, v24
	v_lshl_add_u64 v[24:25], v[24:25], 3, s[48:49]
	v_mov_b32_e32 v24, v200
	v_mov_b32_e32 v25, v201
	v_xor_b32_e32 v28, 0x80000000, v27
	v_mov_b32_e32 v29, v27
	s_nop 0
	v_pk_mul_f32 v[28:29], v[28:29], v[24:25] op_sel:[0,1] op_sel_hi:[1,0]
	s_nop 0
	v_pk_fma_f32 v[24:25], v[26:27], v[24:25], v[28:29] op_sel_hi:[0,1,1]
	v_add_u32_e32 v26, 0x600, v16
	v_ashrrev_i32_e32 v27, 31, v26
	v_lshl_add_u64 v[26:27], v[26:27], 3, s[48:49]
	v_mov_b32_e32 v26, v202
	v_mov_b32_e32 v27, v203
	v_xor_b32_e32 v28, 0x80000000, v71
	v_mov_b32_e32 v29, v71
	s_nop 0
	v_pk_mul_f32 v[28:29], v[26:27], v[28:29] op_sel:[1,0] op_sel_hi:[0,1]
	v_pk_fma_f32 v[26:27], v[26:27], v[70:71], v[28:29] op_sel_hi:[1,0,1]
	v_add_u32_e32 v28, 0x800, v16
	v_ashrrev_i32_e32 v29, 31, v28
	v_lshl_add_u64 v[28:29], v[28:29], 3, s[48:49]
	v_mov_b32_e32 v28, v204
	v_mov_b32_e32 v29, v205
	s_nop 0
	v_pk_mul_f32 v[30:31], v[30:31], v[28:29] op_sel:[0,1] op_sel_hi:[1,0]
	s_nop 0
	v_pk_fma_f32 v[28:29], v[68:69], v[28:29], v[30:31] op_sel_hi:[0,1,1]
	v_add_u32_e32 v30, 0xa00, v16
	v_ashrrev_i32_e32 v31, 31, v30
	v_lshl_add_u64 v[30:31], v[30:31], 3, s[48:49]
	v_mov_b32_e32 v30, v206
	v_mov_b32_e32 v31, v207
	v_mov_b32_e32 v68, v170
	s_nop 0
	v_pk_mul_f32 v[50:51], v[30:31], v[50:51] op_sel:[1,0] op_sel_hi:[0,1]
	v_pk_fma_f32 v[30:31], v[30:31], v[66:67], v[50:51] op_sel_hi:[1,0,1]
	v_add_u32_e32 v50, 0xc00, v16
	v_ashrrev_i32_e32 v51, 31, v50
	v_lshl_add_u64 v[50:51], v[50:51], 3, s[48:49]
	v_mov_b32_e32 v50, v208
	v_mov_b32_e32 v51, v209
	v_xor_b32_e32 v66, 0x80000000, v33
	v_mov_b32_e32 v67, v33
	s_nop 0
	v_pk_mul_f32 v[66:67], v[66:67], v[50:51] op_sel:[0,1] op_sel_hi:[1,0]
	s_nop 0
	v_pk_fma_f32 v[32:33], v[32:33], v[50:51], v[66:67] op_sel_hi:[0,1,1]
	v_add_u32_e32 v50, 0xe00, v16
	v_ashrrev_i32_e32 v51, 31, v50
	v_lshl_add_u64 v[50:51], v[50:51], 3, s[48:49]
	v_mov_b32_e32 v50, v210
	v_mov_b32_e32 v51, v211
	v_xor_b32_e32 v66, 0x80000000, v35
	v_mov_b32_e32 v67, v35
	s_nop 0
	v_pk_mul_f32 v[66:67], v[50:51], v[66:67] op_sel:[1,0] op_sel_hi:[0,1]
	v_pk_fma_f32 v[34:35], v[50:51], v[34:35], v[66:67] op_sel_hi:[1,0,1]
	v_add_u32_e32 v50, 0x1000, v16
	v_ashrrev_i32_e32 v51, 31, v50
	v_lshl_add_u64 v[50:51], v[50:51], 3, s[48:49]
	v_mov_b32_e32 v50, v212
	v_mov_b32_e32 v51, v213
	v_xor_b32_e32 v66, 0x80000000, v37
	v_mov_b32_e32 v67, v37
	s_nop 0
	v_pk_mul_f32 v[66:67], v[66:67], v[50:51] op_sel:[0,1] op_sel_hi:[1,0]
	s_nop 0
	v_pk_fma_f32 v[36:37], v[36:37], v[50:51], v[66:67] op_sel_hi:[0,1,1]
	v_add_u32_e32 v50, 0x1200, v16
	v_ashrrev_i32_e32 v51, 31, v50
	v_lshl_add_u64 v[50:51], v[50:51], 3, s[48:49]
	v_mov_b32_e32 v50, v214
	v_mov_b32_e32 v51, v215
	v_xor_b32_e32 v66, 0x80000000, v41
	v_mov_b32_e32 v67, v41
	v_pk_add_f32 v[70:71], v[20:21], v[36:37]
	v_pk_add_f32 v[20:21], v[20:21], v[36:37] neg_lo:[0,1] neg_hi:[0,1]
	s_nop 0
	v_pk_mul_f32 v[66:67], v[66:67], v[50:51] op_sel:[0,1] op_sel_hi:[1,0]
	s_nop 0
	v_pk_fma_f32 v[40:41], v[40:41], v[50:51], v[66:67] op_sel_hi:[0,1,1]
	v_add_u32_e32 v50, 0x1400, v16
	v_ashrrev_i32_e32 v51, 31, v50
	v_lshl_add_u64 v[50:51], v[50:51], 3, s[48:49]
	v_mov_b32_e32 v50, v216
	v_mov_b32_e32 v51, v217
	v_xor_b32_e32 v66, 0x80000000, v43
	v_mov_b32_e32 v67, v43
	v_pk_add_f32 v[36:37], v[22:23], v[40:41]
	v_pk_add_f32 v[22:23], v[22:23], v[40:41] neg_lo:[0,1] neg_hi:[0,1]
	s_nop 0
	v_pk_mul_f32 v[66:67], v[66:67], v[50:51] op_sel:[0,1] op_sel_hi:[1,0]
	s_nop 0
	v_pk_fma_f32 v[42:43], v[42:43], v[50:51], v[66:67] op_sel_hi:[0,1,1]
	v_add_u32_e32 v50, 0x1600, v16
	v_ashrrev_i32_e32 v51, 31, v50
	v_lshl_add_u64 v[50:51], v[50:51], 3, s[48:49]
	v_mov_b32_e32 v50, v218
	v_mov_b32_e32 v51, v219
	v_xor_b32_e32 v66, 0x80000000, v47
	v_mov_b32_e32 v67, v47
	v_xor_b32_e32 v40, 0x80000000, v23
	v_mov_b32_e32 v41, v22
	s_nop 0
	v_pk_mul_f32 v[66:67], v[66:67], v[50:51] op_sel:[0,1] op_sel_hi:[1,0]
	s_nop 0
	v_pk_fma_f32 v[46:47], v[46:47], v[50:51], v[66:67] op_sel_hi:[0,1,1]
	v_add_u32_e32 v50, 0x1800, v16
	v_ashrrev_i32_e32 v51, 31, v50
	v_lshl_add_u64 v[50:51], v[50:51], 3, s[48:49]
	v_mov_b32_e32 v50, v220
	v_mov_b32_e32 v51, v221
	v_xor_b32_e32 v66, 0x80000000, v45
	v_mov_b32_e32 v67, v45
	s_nop 0
	v_pk_mul_f32 v[66:67], v[66:67], v[50:51] op_sel:[0,1] op_sel_hi:[1,0]
	s_nop 0
	v_pk_fma_f32 v[44:45], v[44:45], v[50:51], v[66:67] op_sel_hi:[0,1,1]
	v_add_u32_e32 v50, 0x1a00, v16
	v_ashrrev_i32_e32 v51, 31, v50
	v_lshl_add_u64 v[50:51], v[50:51], 3, s[48:49]
	v_mov_b32_e32 v50, v222
	v_mov_b32_e32 v51, v223
	v_xor_b32_e32 v66, 0x80000000, v49
	v_mov_b32_e32 v67, v49
	s_nop 0
	v_pk_mul_f32 v[66:67], v[66:67], v[50:51] op_sel:[0,1] op_sel_hi:[1,0]
	s_nop 0
	v_pk_fma_f32 v[48:49], v[48:49], v[50:51], v[66:67] op_sel_hi:[0,1,1]
	v_add_u32_e32 v50, 0x1c00, v16
	v_ashrrev_i32_e32 v51, 31, v50
	v_lshl_add_u64 v[50:51], v[50:51], 3, s[48:49]
	v_mov_b32_e32 v50, v224
	v_mov_b32_e32 v51, v225
	v_xor_b32_e32 v66, 0x80000000, v39
	v_mov_b32_e32 v67, v39
	s_nop 0
	v_pk_mul_f32 v[66:67], v[66:67], v[50:51] op_sel:[0,1] op_sel_hi:[1,0]
	s_nop 0
	v_pk_fma_f32 v[38:39], v[38:39], v[50:51], v[66:67] op_sel_hi:[0,1,1]
	v_add_u32_e32 v50, 0x1e00, v16
	v_ashrrev_i32_e32 v51, 31, v50
	v_lshl_add_u64 v[50:51], v[50:51], 3, s[48:49]
	v_mov_b32_e32 v50, v226
	v_mov_b32_e32 v51, v227
	v_lshlrev_b32_e32 v190, 3, v16
	v_add_u32_e32 v190, 0x11000, v190
	global_load_dwordx2 v[196:197], v190, s[48:49] offset:-4096
	global_load_dwordx2 v[198:199], v190, s[48:49]
	v_add_u32_e32 v190, 0x2000, v190
	global_load_dwordx2 v[200:201], v190, s[48:49] offset:-4096
	global_load_dwordx2 v[202:203], v190, s[48:49]
	v_add_u32_e32 v190, 0x2000, v190
	global_load_dwordx2 v[204:205], v190, s[48:49] offset:-4096
	global_load_dwordx2 v[206:207], v190, s[48:49]
	v_add_u32_e32 v190, 0x2000, v190
	global_load_dwordx2 v[208:209], v190, s[48:49] offset:-4096
	global_load_dwordx2 v[210:211], v190, s[48:49]
	v_add_u32_e32 v190, 0x2000, v190
	global_load_dwordx2 v[212:213], v190, s[48:49] offset:-4096
	global_load_dwordx2 v[214:215], v190, s[48:49]
	v_add_u32_e32 v190, 0x2000, v190
	global_load_dwordx2 v[216:217], v190, s[48:49] offset:-4096
	global_load_dwordx2 v[218:219], v190, s[48:49]
	v_add_u32_e32 v190, 0x2000, v190
	global_load_dwordx2 v[220:221], v190, s[48:49] offset:-4096
	global_load_dwordx2 v[222:223], v190, s[48:49]
	v_add_u32_e32 v190, 0x2000, v190
	global_load_dwordx2 v[224:225], v190, s[48:49] offset:-4096
	global_load_dwordx2 v[226:227], v190, s[48:49]
	v_xor_b32_e32 v66, 0x80000000, v19
	v_mov_b32_e32 v67, v19
	v_mov_b32_e32 v17, v165
	s_nop 0
	v_pk_mul_f32 v[66:67], v[66:67], v[50:51] op_sel:[0,1] op_sel_hi:[1,0]
	s_nop 0
	v_pk_fma_f32 v[18:19], v[18:19], v[50:51], v[66:67] op_sel_hi:[0,1,1]
	v_mov_b32_e32 v50, v166
	v_mov_b32_e32 v17, v167
	v_mov_b32_e32 v66, v168
	v_mov_b32_e32 v17, v169
	s_nop 0
	v_pk_mul_f32 v[40:41], v[40:41], v[68:69] op_sel_hi:[1,0]
	v_mov_b32_e32 v17, v171
	v_pk_fma_f32 v[22:23], v[22:23], v[50:51], v[40:41] op_sel_hi:[1,0,1]
	v_pk_add_f32 v[40:41], v[24:25], v[42:43]
	v_pk_add_f32 v[24:25], v[24:25], v[42:43] neg_lo:[0,1] neg_hi:[0,1]
	s_nop 0
	v_xor_b32_e32 v42, 0x80000000, v25
	v_mov_b32_e32 v43, v24
	v_pk_mul_f32 v[42:43], v[42:43], v[66:67] op_sel_hi:[1,0]
	v_mov_b32_e32 v17, v172
	v_pk_fma_f32 v[24:25], v[24:25], v[66:67], v[42:43] op_sel_hi:[1,0,1]
	v_pk_add_f32 v[42:43], v[26:27], v[46:47]
	v_pk_add_f32 v[26:27], v[26:27], v[46:47] neg_lo:[0,1] neg_hi:[0,1]
	s_nop 0
	v_pk_mul_f32 v[46:47], v[26:27], v[68:69] op_sel_hi:[1,0]
	v_xor_b32_e32 v72, 0x80000000, v27
	v_mov_b32_e32 v73, v26
	v_pk_fma_f32 v[26:27], v[72:73], v[50:51], v[46:47] op_sel_hi:[1,0,1]
	v_pk_add_f32 v[46:47], v[28:29], v[44:45]
	v_pk_add_f32 v[28:29], v[28:29], v[44:45] neg_lo:[0,1] neg_hi:[0,1]
	v_mov_b32_e32 v17, v177
	v_xor_b32_e32 v44, 0x80000000, v29
	v_mov_b32_e32 v45, v28
	v_pk_add_f32 v[28:29], v[30:31], v[48:49]
	v_pk_add_f32 v[30:31], v[30:31], v[48:49] neg_lo:[0,1] neg_hi:[0,1]
	s_nop 0
	v_pk_mul_f32 v[48:49], v[30:31], v[68:69] op_sel_hi:[1,0] neg_lo:[0,1] neg_hi:[0,1]
	v_xor_b32_e32 v72, 0x80000000, v31
	v_mov_b32_e32 v73, v30
	v_pk_fma_f32 v[30:31], v[72:73], v[50:51], v[48:49] op_sel_hi:[1,0,1]
	v_pk_add_f32 v[48:49], v[32:33], v[38:39]
	v_pk_add_f32 v[32:33], v[32:33], v[38:39] neg_lo:[0,1] neg_hi:[0,1]
	s_nop 0
	v_xor_b32_e32 v38, 0x80000000, v33
	v_mov_b32_e32 v39, v32
	v_pk_mul_f32 v[38:39], v[38:39], v[66:67] op_sel_hi:[1,0]
	s_nop 0
	v_pk_fma_f32 v[32:33], v[32:33], v[66:67], v[38:39] op_sel_hi:[1,0,1] neg_lo:[0,1,0] neg_hi:[0,1,0]
	v_pk_add_f32 v[38:39], v[34:35], v[18:19]
	v_pk_add_f32 v[18:19], v[34:35], v[18:19] neg_lo:[0,1] neg_hi:[0,1]
	s_nop 0
	v_xor_b32_e32 v34, 0x80000000, v19
	v_mov_b32_e32 v35, v18
	v_pk_mul_f32 v[34:35], v[34:35], v[68:69] op_sel_hi:[1,0]
	v_mov_b32_e32 v68, v170
	v_pk_fma_f32 v[18:19], v[18:19], v[50:51], v[34:35] op_sel_hi:[1,0,1] neg_lo:[0,1,0] neg_hi:[0,1,0]
	v_pk_add_f32 v[50:51], v[36:37], v[28:29]
	v_pk_add_f32 v[28:29], v[36:37], v[28:29] neg_lo:[0,1] neg_hi:[0,1]
	v_pk_add_f32 v[34:35], v[70:71], v[46:47]
	v_xor_b32_e32 v36, 0x80000000, v29
	v_mov_b32_e32 v37, v28
	v_pk_mul_f32 v[36:37], v[36:37], v[66:67] op_sel_hi:[1,0]
	v_pk_add_f32 v[46:47], v[70:71], v[46:47] neg_lo:[0,1] neg_hi:[0,1]
	v_pk_fma_f32 v[28:29], v[28:29], v[66:67], v[36:37] op_sel_hi:[1,0,1]
	v_pk_add_f32 v[36:37], v[40:41], v[48:49]
	v_pk_add_f32 v[40:41], v[40:41], v[48:49] neg_lo:[0,1] neg_hi:[0,1]
	s_nop 0
	v_xor_b32_e32 v48, 0x80000000, v41
	v_mov_b32_e32 v49, v40
	v_pk_add_f32 v[40:41], v[42:43], v[38:39]
	v_pk_add_f32 v[38:39], v[42:43], v[38:39] neg_lo:[0,1] neg_hi:[0,1]
	s_nop 0
	v_xor_b32_e32 v42, 0x80000000, v39
	v_mov_b32_e32 v43, v38
	v_pk_mul_f32 v[42:43], v[66:67], v[42:43] op_sel_hi:[0,1]
	v_pk_fma_f32 v[38:39], v[38:39], v[66:67], v[42:43] op_sel_hi:[1,0,1] neg_lo:[0,1,0] neg_hi:[0,1,0]
	v_pk_add_f32 v[42:43], v[34:35], v[36:37]
	v_pk_add_f32 v[34:35], v[34:35], v[36:37] neg_lo:[0,1] neg_hi:[0,1]
	v_pk_add_f32 v[36:37], v[50:51], v[40:41]
	v_pk_add_f32 v[40:41], v[50:51], v[40:41] neg_lo:[0,1] neg_hi:[0,1]
	s_nop 0
	v_xor_b32_e32 v50, 0x80000000, v41
	v_mov_b32_e32 v51, v40
	v_pk_add_f32 v[40:41], v[42:43], v[36:37]
	v_pk_add_f32 v[36:37], v[42:43], v[36:37] neg_lo:[0,1] neg_hi:[0,1]
	v_pk_add_f32 v[42:43], v[34:35], v[50:51]
	v_pk_add_f32 v[34:35], v[34:35], v[50:51] neg_lo:[0,1] neg_hi:[0,1]
	v_pk_add_f32 v[50:51], v[46:47], v[48:49]
	v_pk_add_f32 v[46:47], v[46:47], v[48:49] neg_lo:[0,1] neg_hi:[0,1]
	v_pk_add_f32 v[48:49], v[28:29], v[38:39]
	v_pk_add_f32 v[28:29], v[28:29], v[38:39] neg_lo:[0,1] neg_hi:[0,1]
	s_nop 0
	v_xor_b32_e32 v38, 0x80000000, v29
	v_mov_b32_e32 v39, v28
	v_pk_add_f32 v[28:29], v[50:51], v[48:49]
	v_pk_add_f32 v[48:49], v[50:51], v[48:49] neg_lo:[0,1] neg_hi:[0,1]
	v_pk_add_f32 v[50:51], v[46:47], v[38:39]
	v_pk_add_f32 v[38:39], v[46:47], v[38:39] neg_lo:[0,1] neg_hi:[0,1]
	v_pk_add_f32 v[46:47], v[20:21], v[44:45]
	v_pk_add_f32 v[20:21], v[20:21], v[44:45] neg_lo:[0,1] neg_hi:[0,1]
	v_pk_add_f32 v[44:45], v[22:23], v[30:31]
	v_pk_add_f32 v[22:23], v[22:23], v[30:31] neg_lo:[0,1] neg_hi:[0,1]
	s_nop 0
	v_xor_b32_e32 v30, 0x80000000, v23
	v_mov_b32_e32 v31, v22
	v_pk_mul_f32 v[30:31], v[66:67], v[30:31] op_sel_hi:[0,1]
	v_pk_fma_f32 v[22:23], v[66:67], v[22:23], v[30:31] op_sel_hi:[0,1,1]
	v_pk_add_f32 v[30:31], v[24:25], v[32:33]
	v_pk_add_f32 v[24:25], v[24:25], v[32:33] neg_lo:[0,1] neg_hi:[0,1]
	s_nop 0
	v_xor_b32_e32 v32, 0x80000000, v25
	v_mov_b32_e32 v33, v24
	v_pk_add_f32 v[24:25], v[26:27], v[18:19]
	v_pk_add_f32 v[18:19], v[26:27], v[18:19] neg_lo:[0,1] neg_hi:[0,1]
	s_nop 0
	v_xor_b32_e32 v26, 0x80000000, v19
	v_mov_b32_e32 v27, v18
	v_pk_mul_f32 v[26:27], v[66:67], v[26:27] op_sel_hi:[0,1]
	v_pk_fma_f32 v[18:19], v[66:67], v[18:19], v[26:27] op_sel_hi:[0,1,1] neg_lo:[1,0,0] neg_hi:[1,0,0]
	v_pk_add_f32 v[26:27], v[46:47], v[30:31]
	v_pk_add_f32 v[30:31], v[46:47], v[30:31] neg_lo:[0,1] neg_hi:[0,1]
	v_pk_add_f32 v[46:47], v[44:45], v[24:25]
	v_pk_add_f32 v[24:25], v[44:45], v[24:25] neg_lo:[0,1] neg_hi:[0,1]
	v_mov_b32_e32 v66, v168
	v_xor_b32_e32 v44, 0x80000000, v25
	v_mov_b32_e32 v45, v24
	v_pk_add_f32 v[24:25], v[26:27], v[46:47]
	v_pk_add_f32 v[26:27], v[26:27], v[46:47] neg_lo:[0,1] neg_hi:[0,1]
	v_pk_add_f32 v[46:47], v[30:31], v[44:45]
	v_pk_add_f32 v[30:31], v[30:31], v[44:45] neg_lo:[0,1] neg_hi:[0,1]
	v_pk_add_f32 v[44:45], v[20:21], v[32:33]
	v_pk_add_f32 v[20:21], v[20:21], v[32:33] neg_lo:[0,1] neg_hi:[0,1]
	v_pk_add_f32 v[32:33], v[22:23], v[18:19]
	v_pk_add_f32 v[18:19], v[22:23], v[18:19] neg_lo:[0,1] neg_hi:[0,1]
	s_nop 0
	v_xor_b32_e32 v22, 0x80000000, v19
	v_mov_b32_e32 v23, v18
	v_pk_add_f32 v[18:19], v[44:45], v[32:33]
	v_pk_add_f32 v[32:33], v[44:45], v[32:33] neg_lo:[0,1] neg_hi:[0,1]
	v_pk_add_f32 v[44:45], v[20:21], v[22:23]
	v_pk_add_f32 v[20:21], v[20:21], v[22:23] neg_lo:[0,1] neg_hi:[0,1]
	ds_write_b64 v10, v[40:41]
	ds_write_b64 v13, v[24:25]
	ds_write_b64 v15, v[28:29]
	ds_write_b64 v52, v[18:19]
	ds_write_b64 v53, v[42:43]
	ds_write_b64 v54, v[46:47]
	ds_write_b64 v55, v[50:51]
	ds_write_b64 v56, v[44:45]
	ds_write_b64 v57, v[36:37]
	ds_write_b64 v58, v[26:27]
	ds_write_b64 v59, v[48:49]
	ds_write_b64 v60, v[32:33]
	ds_write_b64 v61, v[34:35]
	ds_write_b64 v62, v[30:31]
	ds_write_b64 v63, v[38:39]
	ds_write_b64 v64, v[20:21]
	v_mov_b32_e32 v10, v179
	v_mov_b32_e32 v64, v166
	v_lshlrev_b32_e32 v13, 3, v17
	v_lshlrev_b32_e32 v48, 3, v10
	v_add3_u32 v10, 0, v13, v48
	v_xor_b32_e32 v13, 1, v17
	v_xor_b32_e32 v34, 8, v17
	v_xor_b32_e32 v36, 9, v17
	v_lshlrev_b32_e32 v13, 3, v13
	v_xor_b32_e32 v15, 2, v17
	v_xor_b32_e32 v24, 3, v17
	v_xor_b32_e32 v26, 4, v17
	v_xor_b32_e32 v28, 5, v17
	v_xor_b32_e32 v30, 6, v17
	v_xor_b32_e32 v32, 7, v17
	v_lshlrev_b32_e32 v34, 3, v34
	v_lshlrev_b32_e32 v36, 3, v36
	v_xor_b32_e32 v38, 10, v17
	v_xor_b32_e32 v40, 11, v17
	v_xor_b32_e32 v42, 12, v17
	v_xor_b32_e32 v44, 13, v17
	v_xor_b32_e32 v46, 14, v17
	v_xor_b32_e32 v17, 15, v17
	v_add3_u32 v13, 0, v13, v48
	v_lshlrev_b32_e32 v15, 3, v15
	v_lshlrev_b32_e32 v24, 3, v24
	v_lshlrev_b32_e32 v26, 3, v26
	v_lshlrev_b32_e32 v28, 3, v28
	v_lshlrev_b32_e32 v30, 3, v30
	v_lshlrev_b32_e32 v32, 3, v32
	v_add3_u32 v55, 0, v34, v48
	v_add3_u32 v56, 0, v36, v48
	v_lshlrev_b32_e32 v38, 3, v38
	v_lshlrev_b32_e32 v40, 3, v40
	v_lshlrev_b32_e32 v42, 3, v42
	v_lshlrev_b32_e32 v44, 3, v44
	v_lshlrev_b32_e32 v46, 3, v46
	v_lshlrev_b32_e32 v17, 3, v17
	ds_read_b64 v[18:19], v10
	ds_read_b64 v[20:21], v13
	v_add3_u32 v15, 0, v15, v48
	v_add3_u32 v50, 0, v24, v48
	v_add3_u32 v51, 0, v26, v48
	v_add3_u32 v52, 0, v28, v48
	v_add3_u32 v53, 0, v30, v48
	v_add3_u32 v54, 0, v32, v48
	ds_read_b64 v[34:35], v55
	ds_read_b64 v[36:37], v56
	v_add3_u32 v57, 0, v38, v48
	v_add3_u32 v58, 0, v40, v48
	v_add3_u32 v59, 0, v42, v48
	v_add3_u32 v60, 0, v44, v48
	v_add3_u32 v61, 0, v46, v48
	v_add3_u32 v62, 0, v17, v48
	v_mov_b32_e32 v17, v164
	ds_read_b64 v[22:23], v15
	ds_read_b64 v[24:25], v50
	ds_read_b64 v[26:27], v51
	ds_read_b64 v[28:29], v52
	ds_read_b64 v[30:31], v53
	ds_read_b64 v[32:33], v54
	ds_read_b64 v[38:39], v57
	ds_read_b64 v[40:41], v58
	ds_read_b64 v[42:43], v59
	ds_read_b64 v[44:45], v60
	ds_read_b64 v[46:47], v61
	ds_read_b64 v[48:49], v62
	s_waitcnt lgkmcnt(13)
	v_pk_add_f32 v[70:71], v[18:19], v[34:35]
	v_mov_b32_e32 v17, v165
	v_pk_add_f32 v[18:19], v[18:19], v[34:35] neg_lo:[0,1] neg_hi:[0,1]
	v_mov_b32_e32 v17, v167
	s_waitcnt lgkmcnt(12)
	v_pk_add_f32 v[34:35], v[20:21], v[36:37]
	v_pk_add_f32 v[20:21], v[20:21], v[36:37] neg_lo:[0,1] neg_hi:[0,1]
	v_mov_b32_e32 v17, v169
	v_xor_b32_e32 v36, 0x80000000, v21
	v_mov_b32_e32 v37, v20
	s_nop 0
	v_pk_mul_f32 v[36:37], v[36:37], v[68:69] op_sel_hi:[1,0] neg_lo:[0,1] neg_hi:[0,1]
	v_mov_b32_e32 v17, v171
	v_pk_fma_f32 v[20:21], v[20:21], v[64:65], v[36:37] op_sel_hi:[1,0,1]
	s_waitcnt lgkmcnt(5)
	v_pk_add_f32 v[36:37], v[22:23], v[38:39]
	v_pk_add_f32 v[22:23], v[22:23], v[38:39] neg_lo:[0,1] neg_hi:[0,1]
	s_nop 0
	v_xor_b32_e32 v38, 0x80000000, v23
	v_mov_b32_e32 v39, v22
	v_pk_mul_f32 v[38:39], v[38:39], v[66:67] op_sel_hi:[1,0] neg_lo:[0,1] neg_hi:[0,1]
	v_mov_b32_e32 v17, v172
	v_pk_fma_f32 v[22:23], v[22:23], v[66:67], v[38:39] op_sel_hi:[1,0,1]
	s_waitcnt lgkmcnt(4)
	v_pk_add_f32 v[38:39], v[24:25], v[40:41]
	v_pk_add_f32 v[24:25], v[24:25], v[40:41] neg_lo:[0,1] neg_hi:[0,1]
	s_nop 0
	v_pk_mul_f32 v[40:41], v[24:25], v[68:69] op_sel_hi:[1,0]
	v_xor_b32_e32 v72, 0x80000000, v25
	v_mov_b32_e32 v73, v24
	v_pk_fma_f32 v[24:25], v[72:73], v[64:65], v[40:41] op_sel_hi:[1,0,1] neg_lo:[0,1,0] neg_hi:[0,1,0]
	s_waitcnt lgkmcnt(3)
	v_pk_add_f32 v[40:41], v[26:27], v[42:43]
	v_pk_add_f32 v[26:27], v[26:27], v[42:43] neg_lo:[0,1] neg_hi:[0,1]
	s_nop 0
	v_xor_b32_e32 v73, 0x80000000, v26
	v_mov_b32_e32 v72, v27
	s_waitcnt lgkmcnt(2)
	v_pk_add_f32 v[26:27], v[28:29], v[44:45]
	v_pk_add_f32 v[28:29], v[28:29], v[44:45] neg_lo:[0,1] neg_hi:[0,1]
	s_nop 0
	v_pk_mul_f32 v[42:43], v[28:29], v[68:69] op_sel_hi:[1,0] neg_lo:[0,1] neg_hi:[0,1]
	v_xor_b32_e32 v44, 0x80000000, v29
	v_mov_b32_e32 v45, v28
	v_pk_fma_f32 v[28:29], v[44:45], v[64:65], v[42:43] op_sel_hi:[1,0,1] neg_lo:[0,1,0] neg_hi:[0,1,0]
	s_waitcnt lgkmcnt(1)
	v_pk_add_f32 v[42:43], v[30:31], v[46:47]
	v_pk_add_f32 v[30:31], v[30:31], v[46:47] neg_lo:[0,1] neg_hi:[0,1]
	s_nop 0
	v_xor_b32_e32 v44, 0x80000000, v31
	v_mov_b32_e32 v45, v30
	v_pk_mul_f32 v[44:45], v[44:45], v[66:67] op_sel_hi:[1,0] neg_lo:[0,1] neg_hi:[0,1]
	s_nop 0
	v_pk_fma_f32 v[30:31], v[30:31], v[66:67], v[44:45] op_sel_hi:[1,0,1] neg_lo:[0,1,0] neg_hi:[0,1,0]
	s_waitcnt lgkmcnt(0)
	v_pk_add_f32 v[44:45], v[32:33], v[48:49]
	v_pk_add_f32 v[32:33], v[32:33], v[48:49] neg_lo:[0,1] neg_hi:[0,1]
	v_pk_add_f32 v[48:49], v[34:35], v[26:27]
	v_pk_add_f32 v[26:27], v[34:35], v[26:27] neg_lo:[0,1] neg_hi:[0,1]
	v_xor_b32_e32 v46, 0x80000000, v33
	v_xor_b32_e32 v34, 0x80000000, v27
	v_mov_b32_e32 v35, v26
	v_pk_mul_f32 v[34:35], v[34:35], v[66:67] op_sel_hi:[1,0] neg_lo:[0,1] neg_hi:[0,1]
	v_mov_b32_e32 v47, v32
	v_pk_fma_f32 v[26:27], v[26:27], v[66:67], v[34:35] op_sel_hi:[1,0,1]
	v_pk_add_f32 v[34:35], v[36:37], v[42:43]
	v_pk_add_f32 v[36:37], v[36:37], v[42:43] neg_lo:[0,1] neg_hi:[0,1]
	v_pk_mul_f32 v[46:47], v[46:47], v[68:69] op_sel_hi:[1,0] neg_lo:[0,1] neg_hi:[0,1]
	v_xor_b32_e32 v43, 0x80000000, v36
	v_mov_b32_e32 v42, v37
	v_pk_add_f32 v[36:37], v[38:39], v[44:45]
	v_pk_add_f32 v[38:39], v[38:39], v[44:45] neg_lo:[0,1] neg_hi:[0,1]
	v_pk_fma_f32 v[46:47], v[32:33], v[64:65], v[46:47] op_sel_hi:[1,0,1] neg_lo:[0,1,0] neg_hi:[0,1,0]
	v_xor_b32_e32 v44, 0x80000000, v39
	v_mov_b32_e32 v45, v38
	v_pk_add_f32 v[32:33], v[70:71], v[40:41]
	v_pk_mul_f32 v[44:45], v[44:45], v[66:67] op_sel_hi:[1,0] neg_lo:[0,1] neg_hi:[0,1]
	v_pk_add_f32 v[40:41], v[70:71], v[40:41] neg_lo:[0,1] neg_hi:[0,1]
	v_pk_fma_f32 v[38:39], v[38:39], v[66:67], v[44:45] op_sel_hi:[1,0,1] neg_lo:[0,1,0] neg_hi:[0,1,0]
	v_pk_add_f32 v[44:45], v[32:33], v[34:35]
	v_pk_add_f32 v[32:33], v[32:33], v[34:35] neg_lo:[0,1] neg_hi:[0,1]
	v_pk_add_f32 v[34:35], v[48:49], v[36:37]
	v_pk_add_f32 v[36:37], v[48:49], v[36:37] neg_lo:[0,1] neg_hi:[0,1]
	v_pk_add_f32 v[64:65], v[44:45], v[34:35]
	v_xor_b32_e32 v49, 0x80000000, v36
	v_mov_b32_e32 v48, v37
	v_pk_add_f32 v[36:37], v[44:45], v[34:35] neg_lo:[0,1] neg_hi:[0,1]
	v_pk_add_f32 v[68:69], v[32:33], v[48:49]
	v_pk_add_f32 v[44:45], v[32:33], v[48:49] neg_lo:[0,1] neg_hi:[0,1]
	v_pk_add_f32 v[32:33], v[40:41], v[42:43]
	v_pk_add_f32 v[34:35], v[40:41], v[42:43] neg_lo:[0,1] neg_hi:[0,1]
	v_pk_add_f32 v[40:41], v[26:27], v[38:39]
	v_pk_add_f32 v[26:27], v[26:27], v[38:39] neg_lo:[0,1] neg_hi:[0,1]
	v_pk_add_f32 v[42:43], v[32:33], v[40:41] neg_lo:[0,1] neg_hi:[0,1]
	v_xor_b32_e32 v39, 0x80000000, v26
	v_mov_b32_e32 v38, v27
	v_pk_add_f32 v[26:27], v[32:33], v[40:41]
	v_pk_add_f32 v[40:41], v[20:21], v[28:29]
	v_pk_add_f32 v[20:21], v[20:21], v[28:29] neg_lo:[0,1] neg_hi:[0,1]
	v_pk_add_f32 v[32:33], v[34:35], v[38:39]
	v_xor_b32_e32 v28, 0x80000000, v21
	v_mov_b32_e32 v29, v20
	v_pk_mul_f32 v[28:29], v[66:67], v[28:29] op_sel_hi:[0,1] neg_lo:[1,0] neg_hi:[1,0]
	v_pk_fma_f32 v[20:21], v[66:67], v[20:21], v[28:29] op_sel_hi:[0,1,1]
	v_pk_add_f32 v[28:29], v[22:23], v[30:31]
	v_pk_add_f32 v[22:23], v[22:23], v[30:31] neg_lo:[0,1] neg_hi:[0,1]
	v_pk_add_f32 v[38:39], v[34:35], v[38:39] neg_lo:[0,1] neg_hi:[0,1]
	v_xor_b32_e32 v31, 0x80000000, v22
	v_mov_b32_e32 v30, v23
	v_pk_add_f32 v[22:23], v[24:25], v[46:47]
	v_pk_add_f32 v[24:25], v[24:25], v[46:47] neg_lo:[0,1] neg_hi:[0,1]
	v_pk_add_f32 v[34:35], v[18:19], v[72:73]
	v_xor_b32_e32 v46, 0x80000000, v25
	v_mov_b32_e32 v47, v24
	v_pk_mul_f32 v[46:47], v[66:67], v[46:47] op_sel_hi:[0,1] neg_lo:[1,0] neg_hi:[1,0]
	v_pk_fma_f32 v[24:25], v[66:67], v[24:25], v[46:47] op_sel_hi:[0,1,1] neg_lo:[1,0,0] neg_hi:[1,0,0]
	v_pk_add_f32 v[46:47], v[34:35], v[28:29]
	v_pk_add_f32 v[28:29], v[34:35], v[28:29] neg_lo:[0,1] neg_hi:[0,1]
	v_pk_add_f32 v[34:35], v[40:41], v[22:23]
	v_pk_add_f32 v[22:23], v[40:41], v[22:23] neg_lo:[0,1] neg_hi:[0,1]
	v_pk_add_f32 v[18:19], v[18:19], v[72:73] neg_lo:[0,1] neg_hi:[0,1]
	v_xor_b32_e32 v49, 0x80000000, v22
	v_mov_b32_e32 v48, v23
	v_pk_add_f32 v[66:67], v[28:29], v[48:49]
	v_pk_add_f32 v[48:49], v[28:29], v[48:49] neg_lo:[0,1] neg_hi:[0,1]
	v_pk_add_f32 v[28:29], v[18:19], v[30:31]
	v_pk_add_f32 v[18:19], v[18:19], v[30:31] neg_lo:[0,1] neg_hi:[0,1]
	v_pk_add_f32 v[30:31], v[20:21], v[24:25]
	v_pk_add_f32 v[20:21], v[20:21], v[24:25] neg_lo:[0,1] neg_hi:[0,1]
	v_pk_add_f32 v[22:23], v[46:47], v[34:35]
	v_xor_b32_e32 v25, 0x80000000, v20
	v_add_u32_e32 v20, 0x2000, v16
	v_mov_b32_e32 v24, v21
	v_ashrrev_i32_e32 v21, 31, v20
	v_lshl_add_u64 v[20:21], v[20:21], 3, s[48:49]
	s_waitcnt vmcnt(0)
	v_mov_b32_e32 v20, v196
	v_mov_b32_e32 v21, v197
	v_pk_add_f32 v[40:41], v[46:47], v[34:35] neg_lo:[0,1] neg_hi:[0,1]
	v_pk_add_f32 v[34:35], v[18:19], v[24:25]
	v_pk_add_f32 v[18:19], v[18:19], v[24:25] neg_lo:[0,1] neg_hi:[0,1]
	v_xor_b32_e32 v24, 0x80000000, v65
	v_mov_b32_e32 v25, v65
	v_pk_add_f32 v[70:71], v[28:29], v[30:31]
	v_pk_add_f32 v[46:47], v[28:29], v[30:31] neg_lo:[0,1] neg_hi:[0,1]
	v_xor_b32_e32 v28, 0x80000000, v23
	v_mov_b32_e32 v29, v23
	v_xor_b32_e32 v30, 0x80000000, v69
	v_mov_b32_e32 v31, v69
	s_nop 0
	v_pk_mul_f32 v[24:25], v[24:25], v[20:21] op_sel:[0,1] op_sel_hi:[1,0]
	s_nop 0
	v_pk_fma_f32 v[20:21], v[64:65], v[20:21], v[24:25] op_sel_hi:[0,1,1]
	v_add_u32_e32 v24, 0x2200, v16
	v_ashrrev_i32_e32 v25, 31, v24
	v_lshl_add_u64 v[24:25], v[24:25], 3, s[48:49]
	v_mov_b32_e32 v24, v198
	v_mov_b32_e32 v25, v199
	v_xor_b32_e32 v64, 0x80000000, v67
	v_mov_b32_e32 v65, v67
	s_nop 0
	v_pk_mul_f32 v[28:29], v[24:25], v[28:29] op_sel:[1,0] op_sel_hi:[0,1]
	v_pk_fma_f32 v[22:23], v[24:25], v[22:23], v[28:29] op_sel_hi:[1,0,1]
	v_add_u32_e32 v24, 0x2400, v16
	v_ashrrev_i32_e32 v25, 31, v24
	v_lshl_add_u64 v[24:25], v[24:25], 3, s[48:49]
	v_mov_b32_e32 v24, v200
	v_mov_b32_e32 v25, v201
	v_xor_b32_e32 v28, 0x80000000, v27
	v_mov_b32_e32 v29, v27
	s_nop 0
	v_pk_mul_f32 v[28:29], v[28:29], v[24:25] op_sel:[0,1] op_sel_hi:[1,0]
	s_nop 0
	v_pk_fma_f32 v[24:25], v[26:27], v[24:25], v[28:29] op_sel_hi:[0,1,1]
	v_add_u32_e32 v26, 0x2600, v16
	v_ashrrev_i32_e32 v27, 31, v26
	v_lshl_add_u64 v[26:27], v[26:27], 3, s[48:49]
	v_mov_b32_e32 v26, v202
	v_mov_b32_e32 v27, v203
	v_xor_b32_e32 v28, 0x80000000, v71
	v_mov_b32_e32 v29, v71
	s_nop 0
	v_pk_mul_f32 v[28:29], v[26:27], v[28:29] op_sel:[1,0] op_sel_hi:[0,1]
	v_pk_fma_f32 v[26:27], v[26:27], v[70:71], v[28:29] op_sel_hi:[1,0,1]
	v_add_u32_e32 v28, 0x2800, v16
	v_ashrrev_i32_e32 v29, 31, v28
	v_lshl_add_u64 v[28:29], v[28:29], 3, s[48:49]
	v_mov_b32_e32 v28, v204
	v_mov_b32_e32 v29, v205
	s_nop 0
	v_pk_mul_f32 v[30:31], v[30:31], v[28:29] op_sel:[0,1] op_sel_hi:[1,0]
	s_nop 0
	v_pk_fma_f32 v[28:29], v[68:69], v[28:29], v[30:31] op_sel_hi:[0,1,1]
	v_add_u32_e32 v30, 0x2a00, v16
	v_ashrrev_i32_e32 v31, 31, v30
	v_lshl_add_u64 v[30:31], v[30:31], 3, s[48:49]
	v_mov_b32_e32 v30, v206
	v_mov_b32_e32 v31, v207
	s_nop 0
	v_pk_mul_f32 v[64:65], v[30:31], v[64:65] op_sel:[1,0] op_sel_hi:[0,1]
	v_pk_fma_f32 v[30:31], v[30:31], v[66:67], v[64:65] op_sel_hi:[1,0,1]
	v_add_u32_e32 v64, 0x2c00, v16
	v_ashrrev_i32_e32 v65, 31, v64
	v_lshl_add_u64 v[64:65], v[64:65], 3, s[48:49]
	v_mov_b32_e32 v64, v208
	v_mov_b32_e32 v65, v209
	v_xor_b32_e32 v66, 0x80000000, v33
	v_mov_b32_e32 v67, v33
	s_nop 0
	v_pk_mul_f32 v[66:67], v[66:67], v[64:65] op_sel:[0,1] op_sel_hi:[1,0]
	s_nop 0
	v_pk_fma_f32 v[32:33], v[32:33], v[64:65], v[66:67] op_sel_hi:[0,1,1]
	v_add_u32_e32 v64, 0x2e00, v16
	v_ashrrev_i32_e32 v65, 31, v64
	v_lshl_add_u64 v[64:65], v[64:65], 3, s[48:49]
	v_mov_b32_e32 v64, v210
	v_mov_b32_e32 v65, v211
	v_xor_b32_e32 v66, 0x80000000, v35
	v_mov_b32_e32 v67, v35
	s_nop 0
	v_pk_mul_f32 v[66:67], v[64:65], v[66:67] op_sel:[1,0] op_sel_hi:[0,1]
	v_pk_fma_f32 v[34:35], v[64:65], v[34:35], v[66:67] op_sel_hi:[1,0,1]
	v_add_u32_e32 v64, 0x3000, v16
	v_ashrrev_i32_e32 v65, 31, v64
	v_lshl_add_u64 v[64:65], v[64:65], 3, s[48:49]
	v_mov_b32_e32 v64, v212
	v_mov_b32_e32 v65, v213
	v_xor_b32_e32 v66, 0x80000000, v37
	v_mov_b32_e32 v67, v37
	s_nop 0
	v_pk_mul_f32 v[66:67], v[66:67], v[64:65] op_sel:[0,1] op_sel_hi:[1,0]
	s_nop 0
	v_pk_fma_f32 v[36:37], v[36:37], v[64:65], v[66:67] op_sel_hi:[0,1,1]
	v_add_u32_e32 v64, 0x3200, v16
	v_ashrrev_i32_e32 v65, 31, v64
	v_lshl_add_u64 v[64:65], v[64:65], 3, s[48:49]
	v_mov_b32_e32 v64, v214
	v_mov_b32_e32 v65, v215
	v_xor_b32_e32 v66, 0x80000000, v41
	v_mov_b32_e32 v67, v41
	v_pk_add_f32 v[68:69], v[20:21], v[36:37]
	v_pk_add_f32 v[20:21], v[20:21], v[36:37] neg_lo:[0,1] neg_hi:[0,1]
	s_nop 0
	v_pk_mul_f32 v[66:67], v[66:67], v[64:65] op_sel:[0,1] op_sel_hi:[1,0]
	s_nop 0
	v_pk_fma_f32 v[40:41], v[40:41], v[64:65], v[66:67] op_sel_hi:[0,1,1]
	v_add_u32_e32 v64, 0x3400, v16
	v_ashrrev_i32_e32 v65, 31, v64
	v_lshl_add_u64 v[64:65], v[64:65], 3, s[48:49]
	v_mov_b32_e32 v64, v216
	v_mov_b32_e32 v65, v217
	v_xor_b32_e32 v66, 0x80000000, v43
	v_mov_b32_e32 v67, v43
	v_pk_add_f32 v[36:37], v[22:23], v[40:41]
	v_pk_add_f32 v[22:23], v[22:23], v[40:41] neg_lo:[0,1] neg_hi:[0,1]
	s_nop 0
	v_pk_mul_f32 v[66:67], v[66:67], v[64:65] op_sel:[0,1] op_sel_hi:[1,0]
	s_nop 0
	v_pk_fma_f32 v[42:43], v[42:43], v[64:65], v[66:67] op_sel_hi:[0,1,1]
	v_add_u32_e32 v64, 0x3600, v16
	v_ashrrev_i32_e32 v65, 31, v64
	v_lshl_add_u64 v[64:65], v[64:65], 3, s[48:49]
	v_mov_b32_e32 v64, v218
	v_mov_b32_e32 v65, v219
	v_xor_b32_e32 v66, 0x80000000, v47
	v_mov_b32_e32 v67, v47
	v_xor_b32_e32 v40, 0x80000000, v23
	v_mov_b32_e32 v41, v22
	s_nop 0
	v_pk_mul_f32 v[66:67], v[66:67], v[64:65] op_sel:[0,1] op_sel_hi:[1,0]
	s_nop 0
	v_pk_fma_f32 v[46:47], v[46:47], v[64:65], v[66:67] op_sel_hi:[0,1,1]
	v_add_u32_e32 v64, 0x3800, v16
	v_ashrrev_i32_e32 v65, 31, v64
	v_lshl_add_u64 v[64:65], v[64:65], 3, s[48:49]
	v_mov_b32_e32 v64, v220
	v_mov_b32_e32 v65, v221
	v_xor_b32_e32 v66, 0x80000000, v45
	v_mov_b32_e32 v67, v45
	s_nop 0
	v_pk_mul_f32 v[66:67], v[66:67], v[64:65] op_sel:[0,1] op_sel_hi:[1,0]
	s_nop 0
	v_pk_fma_f32 v[44:45], v[44:45], v[64:65], v[66:67] op_sel_hi:[0,1,1]
	v_add_u32_e32 v64, 0x3a00, v16
	v_ashrrev_i32_e32 v65, 31, v64
	v_lshl_add_u64 v[64:65], v[64:65], 3, s[48:49]
	v_mov_b32_e32 v64, v222
	v_mov_b32_e32 v65, v223
	v_xor_b32_e32 v66, 0x80000000, v49
	v_mov_b32_e32 v67, v49
	s_nop 0
	v_pk_mul_f32 v[66:67], v[66:67], v[64:65] op_sel:[0,1] op_sel_hi:[1,0]
	s_nop 0
	v_pk_fma_f32 v[48:49], v[48:49], v[64:65], v[66:67] op_sel_hi:[0,1,1]
	v_add_u32_e32 v64, 0x3c00, v16
	v_ashrrev_i32_e32 v65, 31, v64
	v_lshl_add_u64 v[64:65], v[64:65], 3, s[48:49]
	v_add_u32_e32 v16, 0x3e00, v16
	v_mov_b32_e32 v64, v224
	v_mov_b32_e32 v65, v225
	v_ashrrev_i32_e32 v17, 31, v16
	v_lshl_add_u64 v[16:17], v[16:17], 3, s[48:49]
	v_mov_b32_e32 v16, v226
	v_mov_b32_e32 v17, v227
	v_xor_b32_e32 v66, 0x80000000, v39
	v_mov_b32_e32 v67, v39
	s_nop 0
	v_pk_mul_f32 v[66:67], v[66:67], v[64:65] op_sel:[0,1] op_sel_hi:[1,0]
	s_nop 0
	v_pk_fma_f32 v[38:39], v[38:39], v[64:65], v[66:67] op_sel_hi:[0,1,1]
	v_xor_b32_e32 v64, 0x80000000, v19
	v_mov_b32_e32 v65, v19
	s_nop 0
	v_pk_mul_f32 v[64:65], v[64:65], v[16:17] op_sel:[0,1] op_sel_hi:[1,0]
	v_mov_b32_e32 v66, v170
	v_pk_fma_f32 v[16:17], v[18:19], v[16:17], v[64:65] op_sel_hi:[0,1,1]
	v_mov_b32_e32 v18, v164
	v_mov_b32_e32 v19, v167
	v_mov_b32_e32 v18, v165
	v_mov_b32_e32 v64, v168
	v_mov_b32_e32 v18, v166
	s_nop 0
	v_mov_b32_e32 v19, v169
	s_nop 0
	v_mov_b32_e32 v19, v171
	v_pk_mul_f32 v[40:41], v[40:41], v[66:67] op_sel_hi:[1,0]
	v_mov_b32_e32 v19, v172
	s_nop 0
	v_pk_fma_f32 v[22:23], v[22:23], v[18:19], v[40:41] op_sel_hi:[1,0,1]
	v_pk_add_f32 v[40:41], v[24:25], v[42:43]
	v_pk_add_f32 v[24:25], v[24:25], v[42:43] neg_lo:[0,1] neg_hi:[0,1]
	s_nop 0
	v_xor_b32_e32 v42, 0x80000000, v25
	v_mov_b32_e32 v43, v24
	v_pk_mul_f32 v[42:43], v[42:43], v[64:65] op_sel_hi:[1,0]
	s_nop 0
	v_pk_fma_f32 v[24:25], v[24:25], v[64:65], v[42:43] op_sel_hi:[1,0,1]
	v_pk_add_f32 v[42:43], v[26:27], v[46:47]
	v_pk_add_f32 v[26:27], v[26:27], v[46:47] neg_lo:[0,1] neg_hi:[0,1]
	s_nop 0
	v_pk_mul_f32 v[46:47], v[26:27], v[66:67] op_sel_hi:[1,0]
	v_xor_b32_e32 v70, 0x80000000, v27
	v_mov_b32_e32 v71, v26
	v_pk_fma_f32 v[26:27], v[70:71], v[18:19], v[46:47] op_sel_hi:[1,0,1]
	v_pk_add_f32 v[46:47], v[28:29], v[44:45]
	v_pk_add_f32 v[28:29], v[28:29], v[44:45] neg_lo:[0,1] neg_hi:[0,1]
	s_nop 0
	v_xor_b32_e32 v44, 0x80000000, v29
	v_mov_b32_e32 v45, v28
	v_pk_add_f32 v[28:29], v[30:31], v[48:49]
	v_pk_add_f32 v[30:31], v[30:31], v[48:49] neg_lo:[0,1] neg_hi:[0,1]
	s_nop 0
	v_pk_mul_f32 v[48:49], v[30:31], v[66:67] op_sel_hi:[1,0] neg_lo:[0,1] neg_hi:[0,1]
	v_xor_b32_e32 v70, 0x80000000, v31
	v_mov_b32_e32 v71, v30
	v_pk_fma_f32 v[30:31], v[70:71], v[18:19], v[48:49] op_sel_hi:[1,0,1]
	v_pk_add_f32 v[48:49], v[32:33], v[38:39]
	v_pk_add_f32 v[32:33], v[32:33], v[38:39] neg_lo:[0,1] neg_hi:[0,1]
	s_nop 0
	v_xor_b32_e32 v38, 0x80000000, v33
	v_mov_b32_e32 v39, v32
	v_pk_mul_f32 v[38:39], v[38:39], v[64:65] op_sel_hi:[1,0]
	s_nop 0
	v_pk_fma_f32 v[32:33], v[32:33], v[64:65], v[38:39] op_sel_hi:[1,0,1] neg_lo:[0,1,0] neg_hi:[0,1,0]
	v_pk_add_f32 v[38:39], v[34:35], v[16:17]
	v_pk_add_f32 v[16:17], v[34:35], v[16:17] neg_lo:[0,1] neg_hi:[0,1]
	s_nop 0
	v_xor_b32_e32 v34, 0x80000000, v17
	v_mov_b32_e32 v35, v16
	v_pk_mul_f32 v[34:35], v[34:35], v[66:67] op_sel_hi:[1,0]
	s_nop 0
	v_pk_fma_f32 v[16:17], v[16:17], v[18:19], v[34:35] op_sel_hi:[1,0,1] neg_lo:[0,1,0] neg_hi:[0,1,0]
	v_pk_add_f32 v[18:19], v[68:69], v[46:47]
	v_pk_add_f32 v[34:35], v[68:69], v[46:47] neg_lo:[0,1] neg_hi:[0,1]
	v_pk_add_f32 v[46:47], v[36:37], v[28:29]
	v_pk_add_f32 v[28:29], v[36:37], v[28:29] neg_lo:[0,1] neg_hi:[0,1]
	s_nop 0
	v_xor_b32_e32 v36, 0x80000000, v29
	v_mov_b32_e32 v37, v28
	v_pk_mul_f32 v[36:37], v[36:37], v[64:65] op_sel_hi:[1,0]
	s_nop 0
	v_pk_fma_f32 v[28:29], v[28:29], v[64:65], v[36:37] op_sel_hi:[1,0,1]
	v_pk_add_f32 v[36:37], v[40:41], v[48:49]
	v_pk_add_f32 v[40:41], v[40:41], v[48:49] neg_lo:[0,1] neg_hi:[0,1]
	s_nop 0
	v_xor_b32_e32 v48, 0x80000000, v41
	v_mov_b32_e32 v49, v40
	v_pk_add_f32 v[40:41], v[42:43], v[38:39]
	v_pk_add_f32 v[38:39], v[42:43], v[38:39] neg_lo:[0,1] neg_hi:[0,1]
	s_nop 0
	v_xor_b32_e32 v42, 0x80000000, v39
	v_mov_b32_e32 v43, v38
	v_pk_mul_f32 v[42:43], v[64:65], v[42:43] op_sel_hi:[0,1]
	v_pk_fma_f32 v[38:39], v[38:39], v[64:65], v[42:43] op_sel_hi:[1,0,1] neg_lo:[0,1,0] neg_hi:[0,1,0]
	v_pk_add_f32 v[42:43], v[18:19], v[36:37]
	v_pk_add_f32 v[18:19], v[18:19], v[36:37] neg_lo:[0,1] neg_hi:[0,1]
	v_pk_add_f32 v[36:37], v[46:47], v[40:41]
	v_pk_add_f32 v[40:41], v[46:47], v[40:41] neg_lo:[0,1] neg_hi:[0,1]
	s_nop 0
	v_xor_b32_e32 v46, 0x80000000, v41
	v_mov_b32_e32 v47, v40
	v_pk_add_f32 v[40:41], v[42:43], v[36:37]
	v_pk_add_f32 v[36:37], v[42:43], v[36:37] neg_lo:[0,1] neg_hi:[0,1]
	v_pk_add_f32 v[42:43], v[18:19], v[46:47]
	v_pk_add_f32 v[18:19], v[18:19], v[46:47] neg_lo:[0,1] neg_hi:[0,1]
	v_pk_add_f32 v[46:47], v[34:35], v[48:49]
	v_pk_add_f32 v[34:35], v[34:35], v[48:49] neg_lo:[0,1] neg_hi:[0,1]
	v_pk_add_f32 v[48:49], v[28:29], v[38:39]
	v_pk_add_f32 v[28:29], v[28:29], v[38:39] neg_lo:[0,1] neg_hi:[0,1]
	s_nop 0
	v_xor_b32_e32 v38, 0x80000000, v29
	v_mov_b32_e32 v39, v28
	v_pk_add_f32 v[28:29], v[46:47], v[48:49]
	v_pk_add_f32 v[46:47], v[46:47], v[48:49] neg_lo:[0,1] neg_hi:[0,1]
	v_pk_add_f32 v[48:49], v[34:35], v[38:39]
	v_pk_add_f32 v[34:35], v[34:35], v[38:39] neg_lo:[0,1] neg_hi:[0,1]
	v_pk_add_f32 v[38:39], v[20:21], v[44:45]
	v_pk_add_f32 v[20:21], v[20:21], v[44:45] neg_lo:[0,1] neg_hi:[0,1]
	v_pk_add_f32 v[44:45], v[22:23], v[30:31]
	v_pk_add_f32 v[22:23], v[22:23], v[30:31] neg_lo:[0,1] neg_hi:[0,1]
	s_nop 0
	v_xor_b32_e32 v30, 0x80000000, v23
	v_mov_b32_e32 v31, v22
	v_pk_mul_f32 v[30:31], v[64:65], v[30:31] op_sel_hi:[0,1]
	v_pk_fma_f32 v[22:23], v[64:65], v[22:23], v[30:31] op_sel_hi:[0,1,1]
	v_pk_add_f32 v[30:31], v[24:25], v[32:33]
	v_pk_add_f32 v[24:25], v[24:25], v[32:33] neg_lo:[0,1] neg_hi:[0,1]
	s_nop 0
	v_xor_b32_e32 v32, 0x80000000, v25
	v_mov_b32_e32 v33, v24
	v_pk_add_f32 v[24:25], v[26:27], v[16:17]
	v_pk_add_f32 v[16:17], v[26:27], v[16:17] neg_lo:[0,1] neg_hi:[0,1]
	s_nop 0
	v_xor_b32_e32 v26, 0x80000000, v17
	v_mov_b32_e32 v27, v16
	v_pk_mul_f32 v[26:27], v[64:65], v[26:27] op_sel_hi:[0,1]
	v_pk_fma_f32 v[16:17], v[64:65], v[16:17], v[26:27] op_sel_hi:[0,1,1] neg_lo:[1,0,0] neg_hi:[1,0,0]
	v_pk_add_f32 v[26:27], v[38:39], v[30:31]
	v_pk_add_f32 v[30:31], v[38:39], v[30:31] neg_lo:[0,1] neg_hi:[0,1]
	v_pk_add_f32 v[38:39], v[44:45], v[24:25]
	v_pk_add_f32 v[24:25], v[44:45], v[24:25] neg_lo:[0,1] neg_hi:[0,1]
	s_nop 0
	v_xor_b32_e32 v44, 0x80000000, v25
	v_mov_b32_e32 v45, v24
	v_pk_add_f32 v[24:25], v[26:27], v[38:39]
	v_pk_add_f32 v[26:27], v[26:27], v[38:39] neg_lo:[0,1] neg_hi:[0,1]
	v_pk_add_f32 v[38:39], v[30:31], v[44:45]
	v_pk_add_f32 v[30:31], v[30:31], v[44:45] neg_lo:[0,1] neg_hi:[0,1]
	v_pk_add_f32 v[44:45], v[20:21], v[32:33]
	v_pk_add_f32 v[20:21], v[20:21], v[32:33] neg_lo:[0,1] neg_hi:[0,1]
	v_pk_add_f32 v[32:33], v[22:23], v[16:17]
	v_pk_add_f32 v[16:17], v[22:23], v[16:17] neg_lo:[0,1] neg_hi:[0,1]
	s_nop 0
	v_xor_b32_e32 v22, 0x80000000, v17
	v_mov_b32_e32 v23, v16
	v_pk_add_f32 v[16:17], v[44:45], v[32:33]
	v_pk_add_f32 v[32:33], v[44:45], v[32:33] neg_lo:[0,1] neg_hi:[0,1]
	v_pk_add_f32 v[44:45], v[20:21], v[22:23]
	v_pk_add_f32 v[20:21], v[20:21], v[22:23] neg_lo:[0,1] neg_hi:[0,1]
	ds_write_b64 v10, v[40:41]
	ds_write_b64 v13, v[24:25]
	ds_write_b64 v15, v[28:29]
	ds_write_b64 v50, v[16:17]
	ds_write_b64 v51, v[42:43]
	ds_write_b64 v52, v[38:39]
	ds_write_b64 v53, v[48:49]
	ds_write_b64 v54, v[44:45]
	ds_write_b64 v55, v[36:37]
	ds_write_b64 v56, v[26:27]
	ds_write_b64 v57, v[46:47]
	ds_write_b64 v58, v[32:33]
	ds_write_b64 v59, v[18:19]
	ds_write_b64 v60, v[30:31]
	ds_write_b64 v61, v[34:35]
	ds_write_b64 v62, v[20:21]
	v_mov_b32_e32 v10, v176
	v_mov_b32_e32 v50, v173
	s_waitcnt lgkmcnt(0)
	s_barrier
	v_mov_b32_e32 v20, v182
	v_add_u32_e32 v13, v50, v10
	v_mov_b32_e32 v21, v183
	v_lshl_add_u32 v13, v13, 3, 0
	ds_read2_b64 v[16:19], v13 offset1:16
	v_xad_u32 v15, v50, 1, v10
	v_lshl_add_u32 v15, v15, 3, 0
	s_waitcnt lgkmcnt(0)
	v_xor_b32_e32 v23, 0x80000000, v16
	v_mov_b32_e32 v22, v17
	v_pk_fma_f32 v[16:17], v[22:23], 0, v[16:17] op_sel_hi:[1,0,1]
	v_pk_fma_f32 v[22:23], v[20:21], s[92:93], v[20:21] op_sel:[1,0,0] op_sel_hi:[0,1,1]
	v_xor_b32_e32 v25, 0x80000000, v18
	v_mov_b32_e32 v24, v19
	v_pk_mul_f32 v[24:25], v[22:23], v[24:25] op_sel:[1,0]
	s_nop 0
	v_pk_fma_f32 v[18:19], v[18:19], v[22:23], v[24:25] op_sel_hi:[1,0,1]
	v_xor_b32_e32 v24, 0x80000000, v23
	v_mov_b32_e32 v25, v23
	v_pk_mul_f32 v[24:25], v[20:21], v[24:25] op_sel:[1,0] op_sel_hi:[0,1]
	v_pk_fma_f32 v[26:27], v[20:21], v[22:23], v[24:25] op_sel_hi:[1,0,1]
	ds_read2_b64 v[22:25], v15 offset0:32 offset1:48
	s_waitcnt lgkmcnt(0)
	v_xor_b32_e32 v29, 0x80000000, v22
	v_mov_b32_e32 v28, v23
	v_pk_mul_f32 v[28:29], v[28:29], v[26:27] op_sel:[0,1]
	s_nop 0
	v_pk_fma_f32 v[22:23], v[22:23], v[26:27], v[28:29] op_sel_hi:[1,0,1]
	v_xor_b32_e32 v28, 0x80000000, v27
	v_mov_b32_e32 v29, v27
	v_pk_mul_f32 v[28:29], v[20:21], v[28:29] op_sel:[1,0] op_sel_hi:[0,1]
	v_pk_fma_f32 v[26:27], v[20:21], v[26:27], v[28:29] op_sel_hi:[1,0,1]
	v_xor_b32_e32 v29, 0x80000000, v24
	v_mov_b32_e32 v28, v25
	v_pk_mul_f32 v[28:29], v[28:29], v[26:27] op_sel:[0,1]
	s_nop 0
	v_pk_fma_f32 v[24:25], v[24:25], v[26:27], v[28:29] op_sel_hi:[1,0,1]
	v_xor_b32_e32 v28, 0x80000000, v27
	v_mov_b32_e32 v29, v27
	v_pk_mul_f32 v[28:29], v[20:21], v[28:29] op_sel:[1,0] op_sel_hi:[0,1]
	v_pk_fma_f32 v[26:27], v[20:21], v[26:27], v[28:29] op_sel_hi:[1,0,1]
	v_xad_u32 v28, v50, 2, v10
	v_lshl_add_u32 v51, v28, 3, 0
	ds_read2_b64 v[28:31], v51 offset0:64 offset1:80
	v_xor_b32_e32 v32, 0x80000000, v27
	v_mov_b32_e32 v33, v27
	v_pk_mul_f32 v[32:33], v[20:21], v[32:33] op_sel:[1,0] op_sel_hi:[0,1]
	s_waitcnt lgkmcnt(0)
	v_xor_b32_e32 v35, 0x80000000, v28
	v_mov_b32_e32 v34, v29
	v_pk_mul_f32 v[34:35], v[34:35], v[26:27] op_sel:[0,1]
	s_nop 0
	v_pk_fma_f32 v[28:29], v[28:29], v[26:27], v[34:35] op_sel_hi:[1,0,1]
	v_pk_fma_f32 v[34:35], v[20:21], v[26:27], v[32:33] op_sel_hi:[1,0,1]
	v_xor_b32_e32 v27, 0x80000000, v30
	v_mov_b32_e32 v26, v31
	v_pk_mul_f32 v[26:27], v[26:27], v[34:35] op_sel:[0,1]
	v_xor_b32_e32 v36, 0x80000000, v35
	v_pk_fma_f32 v[26:27], v[30:31], v[34:35], v[26:27] op_sel_hi:[1,0,1]
	v_xad_u32 v30, v50, 3, v10
	v_lshl_add_u32 v54, v30, 3, 0
	ds_read2_b64 v[30:33], v54 offset0:96 offset1:112
	v_mov_b32_e32 v37, v35
	v_pk_mul_f32 v[36:37], v[20:21], v[36:37] op_sel:[1,0] op_sel_hi:[0,1]
	v_pk_fma_f32 v[34:35], v[20:21], v[34:35], v[36:37] op_sel_hi:[1,0,1]
	s_waitcnt lgkmcnt(0)
	v_xor_b32_e32 v37, 0x80000000, v30
	v_mov_b32_e32 v36, v31
	v_pk_mul_f32 v[36:37], v[36:37], v[34:35] op_sel:[0,1]
	s_nop 0
	v_pk_fma_f32 v[30:31], v[30:31], v[34:35], v[36:37] op_sel_hi:[1,0,1]
	v_xor_b32_e32 v36, 0x80000000, v35
	v_mov_b32_e32 v37, v35
	v_pk_mul_f32 v[36:37], v[20:21], v[36:37] op_sel:[1,0] op_sel_hi:[0,1]
	v_pk_fma_f32 v[34:35], v[20:21], v[34:35], v[36:37] op_sel_hi:[1,0,1]
	v_xor_b32_e32 v37, 0x80000000, v32
	v_mov_b32_e32 v36, v33
	v_pk_mul_f32 v[36:37], v[36:37], v[34:35] op_sel:[0,1]
	s_nop 0
	v_pk_fma_f32 v[32:33], v[32:33], v[34:35], v[36:37] op_sel_hi:[1,0,1]
	v_xor_b32_e32 v36, 0x80000000, v35
	v_mov_b32_e32 v37, v35
	v_pk_mul_f32 v[36:37], v[20:21], v[36:37] op_sel:[1,0] op_sel_hi:[0,1]
	v_pk_fma_f32 v[38:39], v[20:21], v[34:35], v[36:37] op_sel_hi:[1,0,1]
	v_xad_u32 v34, v50, 4, v10
	v_lshl_add_u32 v55, v34, 3, 0
	ds_read2_b64 v[34:37], v55 offset0:128 offset1:144
	v_xor_b32_e32 v40, 0x80000000, v39
	v_mov_b32_e32 v41, v39
	v_pk_mul_f32 v[40:41], v[20:21], v[40:41] op_sel:[1,0] op_sel_hi:[0,1]
	s_waitcnt lgkmcnt(0)
	v_xor_b32_e32 v43, 0x80000000, v34
	v_mov_b32_e32 v42, v35
	v_pk_mul_f32 v[42:43], v[42:43], v[38:39] op_sel:[0,1]
	s_nop 0
	v_pk_fma_f32 v[34:35], v[34:35], v[38:39], v[42:43] op_sel_hi:[1,0,1]
	v_pk_fma_f32 v[42:43], v[20:21], v[38:39], v[40:41] op_sel_hi:[1,0,1]
	v_xor_b32_e32 v39, 0x80000000, v36
	v_mov_b32_e32 v38, v37
	v_pk_mul_f32 v[38:39], v[38:39], v[42:43] op_sel:[0,1]
	v_xor_b32_e32 v44, 0x80000000, v43
	v_pk_fma_f32 v[36:37], v[36:37], v[42:43], v[38:39] op_sel_hi:[1,0,1]
	v_xad_u32 v38, v50, 5, v10
	v_lshl_add_u32 v56, v38, 3, 0
	ds_read2_b64 v[38:41], v56 offset0:160 offset1:176
	v_mov_b32_e32 v45, v43
	v_pk_mul_f32 v[44:45], v[20:21], v[44:45] op_sel:[1,0] op_sel_hi:[0,1]
	v_pk_fma_f32 v[42:43], v[20:21], v[42:43], v[44:45] op_sel_hi:[1,0,1]
	s_waitcnt lgkmcnt(0)
	v_xor_b32_e32 v45, 0x80000000, v38
	v_mov_b32_e32 v44, v39
	v_pk_mul_f32 v[44:45], v[44:45], v[42:43] op_sel:[0,1]
	s_nop 0
	v_pk_fma_f32 v[38:39], v[38:39], v[42:43], v[44:45] op_sel_hi:[1,0,1]
	v_xor_b32_e32 v44, 0x80000000, v43
	v_mov_b32_e32 v45, v43
	v_pk_mul_f32 v[44:45], v[20:21], v[44:45] op_sel:[1,0] op_sel_hi:[0,1]
	v_pk_fma_f32 v[42:43], v[20:21], v[42:43], v[44:45] op_sel_hi:[1,0,1]
	v_xor_b32_e32 v45, 0x80000000, v40
	v_mov_b32_e32 v44, v41
	v_pk_mul_f32 v[44:45], v[44:45], v[42:43] op_sel:[0,1]
	s_nop 0
	v_pk_fma_f32 v[40:41], v[40:41], v[42:43], v[44:45] op_sel_hi:[1,0,1]
	v_xor_b32_e32 v44, 0x80000000, v43
	v_mov_b32_e32 v45, v43
	v_pk_mul_f32 v[44:45], v[20:21], v[44:45] op_sel:[1,0] op_sel_hi:[0,1]
	v_pk_fma_f32 v[42:43], v[20:21], v[42:43], v[44:45] op_sel_hi:[1,0,1]
	v_xad_u32 v44, v50, 6, v10
	v_lshl_add_u32 v57, v44, 3, 0
	ds_read2_b64 v[44:47], v57 offset0:192 offset1:208
	v_xor_b32_e32 v48, 0x80000000, v43
	v_mov_b32_e32 v49, v43
	v_pk_mul_f32 v[48:49], v[20:21], v[48:49] op_sel:[1,0] op_sel_hi:[0,1]
	s_waitcnt lgkmcnt(0)
	v_xor_b32_e32 v53, 0x80000000, v44
	v_mov_b32_e32 v52, v45
	v_pk_mul_f32 v[52:53], v[52:53], v[42:43] op_sel:[0,1]
	s_nop 0
	v_pk_fma_f32 v[44:45], v[44:45], v[42:43], v[52:53] op_sel_hi:[1,0,1]
	v_pk_fma_f32 v[52:53], v[20:21], v[42:43], v[48:49] op_sel_hi:[1,0,1]
	v_xor_b32_e32 v43, 0x80000000, v46
	v_mov_b32_e32 v42, v47
	v_pk_mul_f32 v[42:43], v[42:43], v[52:53] op_sel:[0,1]
	v_xor_b32_e32 v60, 0x80000000, v53
	v_pk_fma_f32 v[42:43], v[46:47], v[52:53], v[42:43] op_sel_hi:[1,0,1]
	v_xad_u32 v46, v50, 7, v10
	v_lshl_add_u32 v58, v46, 3, 0
	ds_read2_b64 v[46:49], v58 offset0:224 offset1:240
	v_mov_b32_e32 v61, v53
	v_pk_mul_f32 v[60:61], v[20:21], v[60:61] op_sel:[1,0] op_sel_hi:[0,1]
	v_pk_fma_f32 v[52:53], v[20:21], v[52:53], v[60:61] op_sel_hi:[1,0,1]
	s_waitcnt lgkmcnt(0)
	v_xor_b32_e32 v61, 0x80000000, v46
	v_mov_b32_e32 v60, v47
	v_pk_mul_f32 v[60:61], v[60:61], v[52:53] op_sel:[0,1]
	s_nop 0
	v_pk_fma_f32 v[46:47], v[46:47], v[52:53], v[60:61] op_sel_hi:[1,0,1]
	v_xor_b32_e32 v60, 0x80000000, v53
	v_mov_b32_e32 v61, v53
	v_pk_mul_f32 v[60:61], v[20:21], v[60:61] op_sel:[1,0] op_sel_hi:[0,1]
	v_pk_fma_f32 v[52:53], v[20:21], v[52:53], v[60:61] op_sel_hi:[1,0,1]
	v_xor_b32_e32 v61, 0x80000000, v48
	v_mov_b32_e32 v60, v49
	v_pk_mul_f32 v[60:61], v[60:61], v[52:53] op_sel:[0,1]
	s_nop 0
	v_pk_fma_f32 v[48:49], v[48:49], v[52:53], v[60:61] op_sel_hi:[1,0,1]
	v_xor_b32_e32 v60, 0x80000000, v53
	v_mov_b32_e32 v61, v53
	v_pk_mul_f32 v[60:61], v[20:21], v[60:61] op_sel:[1,0] op_sel_hi:[0,1]
	v_pk_fma_f32 v[64:65], v[20:21], v[52:53], v[60:61] op_sel_hi:[1,0,1]
	v_xad_u32 v52, v50, 8, v10
	v_lshl_add_u32 v52, v52, 3, 0
	v_add_u32_e32 v59, 0x800, v52
	ds_read2_b64 v[60:63], v59 offset1:16
	v_xor_b32_e32 v52, 0x80000000, v65
	v_mov_b32_e32 v53, v65
	v_pk_mul_f32 v[66:67], v[20:21], v[52:53] op_sel:[1,0] op_sel_hi:[0,1]
	v_pk_fma_f32 v[66:67], v[20:21], v[64:65], v[66:67] op_sel_hi:[1,0,1]
	s_waitcnt lgkmcnt(0)
	v_xor_b32_e32 v53, 0x80000000, v60
	v_mov_b32_e32 v52, v61
	v_pk_mul_f32 v[52:53], v[52:53], v[64:65] op_sel:[0,1]
	v_xor_b32_e32 v68, 0x80000000, v67
	v_pk_fma_f32 v[52:53], v[60:61], v[64:65], v[52:53] op_sel_hi:[1,0,1]
	v_xor_b32_e32 v61, 0x80000000, v62
	v_mov_b32_e32 v60, v63
	v_pk_mul_f32 v[60:61], v[60:61], v[66:67] op_sel:[0,1]
	v_mov_b32_e32 v69, v67
	v_pk_fma_f32 v[70:71], v[62:63], v[66:67], v[60:61] op_sel_hi:[1,0,1]
	v_xad_u32 v60, v50, 9, v10
	v_lshl_add_u32 v60, v60, 3, 0
	v_add_u32_e32 v60, 0x800, v60
	ds_read2_b64 v[62:65], v60 offset0:32 offset1:48
	v_pk_mul_f32 v[68:69], v[20:21], v[68:69] op_sel:[1,0] op_sel_hi:[0,1]
	v_pk_fma_f32 v[66:67], v[20:21], v[66:67], v[68:69] op_sel_hi:[1,0,1]
	s_waitcnt lgkmcnt(0)
	v_xor_b32_e32 v69, 0x80000000, v62
	v_mov_b32_e32 v68, v63
	v_pk_mul_f32 v[68:69], v[68:69], v[66:67] op_sel:[0,1]
	s_nop 0
	v_pk_fma_f32 v[72:73], v[62:63], v[66:67], v[68:69] op_sel_hi:[1,0,1]
	v_xor_b32_e32 v62, 0x80000000, v67
	v_mov_b32_e32 v63, v67
	v_pk_mul_f32 v[62:63], v[20:21], v[62:63] op_sel:[1,0] op_sel_hi:[0,1]
	v_pk_fma_f32 v[62:63], v[20:21], v[66:67], v[62:63] op_sel_hi:[1,0,1]
	v_xor_b32_e32 v67, 0x80000000, v64
	v_mov_b32_e32 v66, v65
	v_pk_mul_f32 v[66:67], v[66:67], v[62:63] op_sel:[0,1]
	s_nop 0
	v_pk_fma_f32 v[74:75], v[64:65], v[62:63], v[66:67] op_sel_hi:[1,0,1]
	v_xor_b32_e32 v64, 0x80000000, v63
	v_mov_b32_e32 v65, v63
	v_pk_mul_f32 v[64:65], v[20:21], v[64:65] op_sel:[1,0] op_sel_hi:[0,1]
	v_pk_fma_f32 v[66:67], v[20:21], v[62:63], v[64:65] op_sel_hi:[1,0,1]
	v_xad_u32 v61, v50, 10, v10
	v_lshl_add_u32 v61, v61, 3, 0
	v_add_u32_e32 v61, 0x800, v61
	ds_read2_b64 v[62:65], v61 offset0:64 offset1:80
	v_xor_b32_e32 v68, 0x80000000, v67
	v_mov_b32_e32 v69, v67
	v_pk_mul_f32 v[68:69], v[20:21], v[68:69] op_sel:[1,0] op_sel_hi:[0,1]
	v_pk_fma_f32 v[68:69], v[20:21], v[66:67], v[68:69] op_sel_hi:[1,0,1]
	s_waitcnt lgkmcnt(0)
	v_xor_b32_e32 v77, 0x80000000, v62
	v_mov_b32_e32 v76, v63
	v_pk_mul_f32 v[76:77], v[76:77], v[66:67] op_sel:[0,1]
	v_xor_b32_e32 v80, 0x80000000, v69
	v_pk_fma_f32 v[76:77], v[62:63], v[66:67], v[76:77] op_sel_hi:[1,0,1]
	v_xor_b32_e32 v63, 0x80000000, v64
	v_mov_b32_e32 v62, v65
	v_pk_mul_f32 v[62:63], v[62:63], v[68:69] op_sel:[0,1]
	v_mov_b32_e32 v81, v69
	v_pk_fma_f32 v[78:79], v[64:65], v[68:69], v[62:63] op_sel_hi:[1,0,1]
	v_xad_u32 v62, v50, 11, v10
	v_lshl_add_u32 v62, v62, 3, 0
	v_add_u32_e32 v62, 0x800, v62
	ds_read2_b64 v[64:67], v62 offset0:96 offset1:112
	v_pk_mul_f32 v[80:81], v[20:21], v[80:81] op_sel:[1,0] op_sel_hi:[0,1]
	v_pk_fma_f32 v[68:69], v[20:21], v[68:69], v[80:81] op_sel_hi:[1,0,1]
	s_waitcnt lgkmcnt(0)
	v_xor_b32_e32 v81, 0x80000000, v64
	v_mov_b32_e32 v80, v65
	v_pk_mul_f32 v[80:81], v[80:81], v[68:69] op_sel:[0,1]
	s_nop 0
	v_pk_fma_f32 v[80:81], v[64:65], v[68:69], v[80:81] op_sel_hi:[1,0,1]
	v_xor_b32_e32 v64, 0x80000000, v69
	v_mov_b32_e32 v65, v69
	v_pk_mul_f32 v[64:65], v[20:21], v[64:65] op_sel:[1,0] op_sel_hi:[0,1]
	v_pk_fma_f32 v[64:65], v[20:21], v[68:69], v[64:65] op_sel_hi:[1,0,1]
	v_xor_b32_e32 v69, 0x80000000, v66
	v_mov_b32_e32 v68, v67
	v_pk_mul_f32 v[68:69], v[68:69], v[64:65] op_sel:[0,1]
	s_nop 0
	v_pk_fma_f32 v[82:83], v[66:67], v[64:65], v[68:69] op_sel_hi:[1,0,1]
	v_xor_b32_e32 v66, 0x80000000, v65
	v_mov_b32_e32 v67, v65
	v_pk_mul_f32 v[66:67], v[20:21], v[66:67] op_sel:[1,0] op_sel_hi:[0,1]
	v_pk_fma_f32 v[68:69], v[20:21], v[64:65], v[66:67] op_sel_hi:[1,0,1]
	v_xad_u32 v63, v50, 12, v10
	v_lshl_add_u32 v63, v63, 3, 0
	v_add_u32_e32 v63, 0x800, v63
	ds_read2_b64 v[64:67], v63 offset0:128 offset1:144
	v_xor_b32_e32 v84, 0x80000000, v69
	v_mov_b32_e32 v85, v69
	v_pk_mul_f32 v[84:85], v[20:21], v[84:85] op_sel:[1,0] op_sel_hi:[0,1]
	v_pk_fma_f32 v[84:85], v[20:21], v[68:69], v[84:85] op_sel_hi:[1,0,1]
	s_waitcnt lgkmcnt(0)
	v_xor_b32_e32 v87, 0x80000000, v64
	v_mov_b32_e32 v86, v65
	v_pk_mul_f32 v[86:87], v[86:87], v[68:69] op_sel:[0,1]
	v_xor_b32_e32 v90, 0x80000000, v85
	v_pk_fma_f32 v[86:87], v[64:65], v[68:69], v[86:87] op_sel_hi:[1,0,1]
	v_xor_b32_e32 v65, 0x80000000, v66
	v_mov_b32_e32 v64, v67
	v_pk_mul_f32 v[64:65], v[64:65], v[84:85] op_sel:[0,1]
	v_mov_b32_e32 v91, v85
	v_pk_fma_f32 v[88:89], v[66:67], v[84:85], v[64:65] op_sel_hi:[1,0,1]
	v_xad_u32 v64, v50, 13, v10
	v_lshl_add_u32 v64, v64, 3, 0
	v_add_u32_e32 v64, 0x800, v64
	ds_read2_b64 v[66:69], v64 offset0:160 offset1:176
	v_pk_mul_f32 v[90:91], v[20:21], v[90:91] op_sel:[1,0] op_sel_hi:[0,1]
	v_pk_fma_f32 v[84:85], v[20:21], v[84:85], v[90:91] op_sel_hi:[1,0,1]
	s_waitcnt lgkmcnt(0)
	v_xor_b32_e32 v91, 0x80000000, v66
	v_mov_b32_e32 v90, v67
	v_pk_mul_f32 v[90:91], v[90:91], v[84:85] op_sel:[0,1]
	s_nop 0
	v_pk_fma_f32 v[90:91], v[66:67], v[84:85], v[90:91] op_sel_hi:[1,0,1]
	v_xor_b32_e32 v66, 0x80000000, v85
	v_mov_b32_e32 v67, v85
	v_pk_mul_f32 v[66:67], v[20:21], v[66:67] op_sel:[1,0] op_sel_hi:[0,1]
	v_pk_fma_f32 v[66:67], v[20:21], v[84:85], v[66:67] op_sel_hi:[1,0,1]
	v_xor_b32_e32 v85, 0x80000000, v68
	v_mov_b32_e32 v84, v69
	v_pk_mul_f32 v[84:85], v[84:85], v[66:67] op_sel:[0,1]
	s_nop 0
	v_pk_fma_f32 v[84:85], v[68:69], v[66:67], v[84:85] op_sel_hi:[1,0,1]
	v_xor_b32_e32 v68, 0x80000000, v67
	v_mov_b32_e32 v69, v67
	v_pk_mul_f32 v[68:69], v[20:21], v[68:69] op_sel:[1,0] op_sel_hi:[0,1]
	v_pk_fma_f32 v[92:93], v[20:21], v[66:67], v[68:69] op_sel_hi:[1,0,1]
	v_xad_u32 v65, v50, 14, v10
	v_lshl_add_u32 v65, v65, 3, 0
	v_add_u32_e32 v65, 0x800, v65
	ds_read2_b64 v[66:69], v65 offset0:192 offset1:208
	v_xor_b32_e32 v94, 0x80000000, v93
	v_mov_b32_e32 v95, v93
	v_pk_mul_f32 v[94:95], v[20:21], v[94:95] op_sel:[1,0] op_sel_hi:[0,1]
	v_xad_u32 v10, v50, 15, v10
	s_waitcnt lgkmcnt(0)
	v_xor_b32_e32 v97, 0x80000000, v66
	v_mov_b32_e32 v96, v67
	v_pk_mul_f32 v[96:97], v[96:97], v[92:93] op_sel:[0,1]
	v_lshl_add_u32 v10, v10, 3, 0
	v_pk_fma_f32 v[96:97], v[66:67], v[92:93], v[96:97] op_sel_hi:[1,0,1]
	v_pk_fma_f32 v[92:93], v[20:21], v[92:93], v[94:95] op_sel_hi:[1,0,1]
	v_xor_b32_e32 v67, 0x80000000, v68
	v_mov_b32_e32 v66, v69
	v_pk_mul_f32 v[66:67], v[66:67], v[92:93] op_sel:[0,1]
	v_add_u32_e32 v101, 0x800, v10
	v_pk_fma_f32 v[94:95], v[68:69], v[92:93], v[66:67] op_sel_hi:[1,0,1]
	ds_read2_b64 v[66:69], v101 offset0:224 offset1:240
	v_xor_b32_e32 v98, 0x80000000, v93
	v_mov_b32_e32 v99, v93
	v_pk_mul_f32 v[98:99], v[20:21], v[98:99] op_sel:[1,0] op_sel_hi:[0,1]
	v_pk_fma_f32 v[92:93], v[20:21], v[92:93], v[98:99] op_sel_hi:[1,0,1]
	s_waitcnt lgkmcnt(0)
	v_xor_b32_e32 v99, 0x80000000, v66
	v_mov_b32_e32 v98, v67
	v_pk_mul_f32 v[98:99], v[98:99], v[92:93] op_sel:[0,1]
	s_nop 0
	v_pk_fma_f32 v[66:67], v[66:67], v[92:93], v[98:99] op_sel_hi:[1,0,1]
	v_xor_b32_e32 v98, 0x80000000, v93
	v_mov_b32_e32 v99, v93
	v_pk_mul_f32 v[98:99], v[20:21], v[98:99] op_sel:[1,0] op_sel_hi:[0,1]
	v_pk_fma_f32 v[20:21], v[20:21], v[92:93], v[98:99] op_sel_hi:[1,0,1]
	v_xor_b32_e32 v93, 0x80000000, v68
	v_mov_b32_e32 v92, v69
	v_pk_mul_f32 v[92:93], v[92:93], v[20:21] op_sel:[0,1]
	s_nop 0
	v_pk_fma_f32 v[68:69], v[68:69], v[20:21], v[92:93] op_sel_hi:[1,0,1]
	v_mov_b32_e32 v10, v164
	v_pk_add_f32 v[104:105], v[16:17], v[52:53]
	v_pk_add_f32 v[16:17], v[16:17], v[52:53] neg_lo:[0,1] neg_hi:[0,1]
	v_pk_add_f32 v[52:53], v[18:19], v[70:71]
	v_pk_add_f32 v[18:19], v[18:19], v[70:71] neg_lo:[0,1] neg_hi:[0,1]
	v_mov_b32_e32 v92, v165
	v_mov_b32_e32 v20, v166
	v_mov_b32_e32 v98, v167
	v_mov_b32_e32 v10, v168
	v_mov_b32_e32 v100, v169
	v_mov_b32_e32 v50, v170
	v_mov_b32_e32 v102, v171
	v_xor_b32_e32 v70, 0x80000000, v19
	v_mov_b32_e32 v71, v18
	v_mov_b32_e32 v21, v172
	v_pk_mul_f32 v[70:71], v[102:103], v[70:71] op_sel_hi:[0,1]
	v_pk_fma_f32 v[18:19], v[92:93], v[18:19], v[70:71] op_sel_hi:[0,1,1]
	v_pk_add_f32 v[70:71], v[22:23], v[72:73]
	v_pk_add_f32 v[22:23], v[22:23], v[72:73] neg_lo:[0,1] neg_hi:[0,1]
	s_nop 0
	v_xor_b32_e32 v72, 0x80000000, v23
	v_mov_b32_e32 v73, v22
	v_pk_mul_f32 v[72:73], v[50:51], v[72:73] op_sel_hi:[0,1]
	v_pk_fma_f32 v[22:23], v[20:21], v[22:23], v[72:73] op_sel_hi:[0,1,1]
	v_pk_add_f32 v[72:73], v[24:25], v[74:75]
	v_pk_add_f32 v[24:25], v[24:25], v[74:75] neg_lo:[0,1] neg_hi:[0,1]
	s_nop 0
	v_xor_b32_e32 v74, 0x80000000, v25
	v_mov_b32_e32 v75, v24
	v_pk_mul_f32 v[74:75], v[100:101], v[74:75] op_sel_hi:[0,1]
	v_pk_fma_f32 v[24:25], v[98:99], v[24:25], v[74:75] op_sel_hi:[0,1,1]
	v_pk_add_f32 v[74:75], v[28:29], v[76:77]
	v_pk_add_f32 v[28:29], v[28:29], v[76:77] neg_lo:[0,1] neg_hi:[0,1]
	s_nop 0
	v_xor_b32_e32 v76, 0x80000000, v29
	v_mov_b32_e32 v77, v28
	v_pk_mul_f32 v[76:77], v[10:11], v[76:77] op_sel_hi:[0,1]
	v_pk_fma_f32 v[28:29], v[10:11], v[28:29], v[76:77] op_sel_hi:[0,1,1]
	v_pk_add_f32 v[76:77], v[26:27], v[78:79]
	v_pk_add_f32 v[26:27], v[26:27], v[78:79] neg_lo:[0,1] neg_hi:[0,1]
	s_nop 0
	v_xor_b32_e32 v78, 0x80000000, v27
	v_mov_b32_e32 v79, v26
	v_pk_mul_f32 v[78:79], v[98:99], v[78:79] op_sel_hi:[0,1]
	v_pk_fma_f32 v[26:27], v[100:101], v[26:27], v[78:79] op_sel_hi:[0,1,1]
	v_pk_add_f32 v[78:79], v[30:31], v[80:81]
	v_pk_add_f32 v[30:31], v[30:31], v[80:81] neg_lo:[0,1] neg_hi:[0,1]
	s_nop 0
	v_xor_b32_e32 v80, 0x80000000, v31
	v_mov_b32_e32 v81, v30
	v_pk_mul_f32 v[80:81], v[20:21], v[80:81] op_sel_hi:[0,1]
	v_pk_fma_f32 v[30:31], v[50:51], v[30:31], v[80:81] op_sel_hi:[0,1,1]
	v_pk_add_f32 v[80:81], v[32:33], v[82:83]
	v_pk_add_f32 v[32:33], v[32:33], v[82:83] neg_lo:[0,1] neg_hi:[0,1]
	s_nop 0
	v_xor_b32_e32 v82, 0x80000000, v33
	v_mov_b32_e32 v83, v32
	v_pk_mul_f32 v[82:83], v[92:93], v[82:83] op_sel_hi:[0,1]
	v_pk_fma_f32 v[32:33], v[102:103], v[32:33], v[82:83] op_sel_hi:[0,1,1]
	v_pk_add_f32 v[82:83], v[34:35], v[86:87]
	v_pk_add_f32 v[34:35], v[34:35], v[86:87] neg_lo:[0,1] neg_hi:[0,1]
	s_nop 0
	v_xor_b32_e32 v86, 0x80000000, v35
	v_mov_b32_e32 v87, v34
	v_pk_add_f32 v[34:35], v[36:37], v[88:89]
	v_pk_add_f32 v[36:37], v[36:37], v[88:89] neg_lo:[0,1] neg_hi:[0,1]
	s_nop 0
	v_xor_b32_e32 v88, 0x80000000, v37
	v_mov_b32_e32 v89, v36
	v_pk_mul_f32 v[88:89], v[92:93], v[88:89] op_sel_hi:[0,1]
	v_pk_fma_f32 v[36:37], v[102:103], v[36:37], v[88:89] op_sel_hi:[0,1,1] neg_lo:[1,0,0] neg_hi:[1,0,0]
	v_pk_add_f32 v[88:89], v[38:39], v[90:91]
	v_pk_add_f32 v[38:39], v[38:39], v[90:91] neg_lo:[0,1] neg_hi:[0,1]
	s_nop 0
	v_xor_b32_e32 v90, 0x80000000, v39
	v_mov_b32_e32 v91, v38
	v_pk_mul_f32 v[90:91], v[20:21], v[90:91] op_sel_hi:[0,1]
	v_pk_fma_f32 v[38:39], v[50:51], v[38:39], v[90:91] op_sel_hi:[0,1,1] neg_lo:[1,0,0] neg_hi:[1,0,0]
	v_pk_add_f32 v[90:91], v[40:41], v[84:85]
	v_pk_add_f32 v[40:41], v[40:41], v[84:85] neg_lo:[0,1] neg_hi:[0,1]
	s_nop 0
	v_xor_b32_e32 v84, 0x80000000, v41
	v_mov_b32_e32 v85, v40
	v_pk_mul_f32 v[84:85], v[98:99], v[84:85] op_sel_hi:[0,1]
	v_pk_fma_f32 v[40:41], v[100:101], v[40:41], v[84:85] op_sel_hi:[0,1,1] neg_lo:[1,0,0] neg_hi:[1,0,0]
	v_pk_add_f32 v[84:85], v[44:45], v[96:97]
	v_pk_add_f32 v[44:45], v[44:45], v[96:97] neg_lo:[0,1] neg_hi:[0,1]
	s_nop 0
	v_xor_b32_e32 v96, 0x80000000, v45
	v_mov_b32_e32 v97, v44
	v_pk_mul_f32 v[96:97], v[10:11], v[96:97] op_sel_hi:[0,1]
	v_pk_fma_f32 v[44:45], v[10:11], v[44:45], v[96:97] op_sel_hi:[0,1,1] neg_lo:[1,0,0] neg_hi:[1,0,0]
	v_pk_add_f32 v[96:97], v[42:43], v[94:95]
	v_pk_add_f32 v[42:43], v[42:43], v[94:95] neg_lo:[0,1] neg_hi:[0,1]
	s_nop 0
	v_xor_b32_e32 v94, 0x80000000, v43
	v_mov_b32_e32 v95, v42
	v_pk_mul_f32 v[94:95], v[100:101], v[94:95] op_sel_hi:[0,1]
	v_pk_fma_f32 v[42:43], v[98:99], v[42:43], v[94:95] op_sel_hi:[0,1,1] neg_lo:[1,0,0] neg_hi:[1,0,0]
	v_pk_add_f32 v[94:95], v[46:47], v[66:67]
	v_pk_add_f32 v[46:47], v[46:47], v[66:67] neg_lo:[0,1] neg_hi:[0,1]
	s_nop 0
	v_xor_b32_e32 v66, 0x80000000, v47
	v_mov_b32_e32 v67, v46
	v_pk_mul_f32 v[66:67], v[50:51], v[66:67] op_sel_hi:[0,1]
	v_pk_fma_f32 v[46:47], v[20:21], v[46:47], v[66:67] op_sel_hi:[0,1,1] neg_lo:[1,0,0] neg_hi:[1,0,0]
	v_pk_add_f32 v[66:67], v[48:49], v[68:69]
	v_pk_add_f32 v[48:49], v[48:49], v[68:69] neg_lo:[0,1] neg_hi:[0,1]
	s_nop 0
	v_xor_b32_e32 v68, 0x80000000, v49
	v_mov_b32_e32 v69, v48
	v_pk_mul_f32 v[68:69], v[102:103], v[68:69] op_sel_hi:[0,1]
	v_pk_fma_f32 v[48:49], v[92:93], v[48:49], v[68:69] op_sel_hi:[0,1,1] neg_lo:[1,0,0] neg_hi:[1,0,0]
	v_pk_add_f32 v[92:93], v[52:53], v[34:35]
	v_pk_add_f32 v[34:35], v[52:53], v[34:35] neg_lo:[0,1] neg_hi:[0,1]
	v_pk_add_f32 v[68:69], v[104:105], v[82:83]
	v_xor_b32_e32 v52, 0x80000000, v35
	v_mov_b32_e32 v53, v34
	v_pk_mul_f32 v[52:53], v[50:51], v[52:53] op_sel_hi:[0,1]
	v_pk_fma_f32 v[34:35], v[20:21], v[34:35], v[52:53] op_sel_hi:[0,1,1]
	v_pk_add_f32 v[52:53], v[70:71], v[88:89]
	v_pk_add_f32 v[70:71], v[70:71], v[88:89] neg_lo:[0,1] neg_hi:[0,1]
	v_pk_add_f32 v[82:83], v[104:105], v[82:83] neg_lo:[0,1] neg_hi:[0,1]
	v_xor_b32_e32 v88, 0x80000000, v71
	v_mov_b32_e32 v89, v70
	v_pk_mul_f32 v[88:89], v[10:11], v[88:89] op_sel_hi:[0,1]
	v_pk_fma_f32 v[70:71], v[10:11], v[70:71], v[88:89] op_sel_hi:[0,1,1]
	v_pk_add_f32 v[88:89], v[72:73], v[90:91]
	v_pk_add_f32 v[72:73], v[72:73], v[90:91] neg_lo:[0,1] neg_hi:[0,1]
	s_nop 0
	v_xor_b32_e32 v90, 0x80000000, v73
	v_mov_b32_e32 v91, v72
	v_pk_mul_f32 v[90:91], v[20:21], v[90:91] op_sel_hi:[0,1]
	v_pk_fma_f32 v[72:73], v[50:51], v[72:73], v[90:91] op_sel_hi:[0,1,1]
	v_pk_add_f32 v[90:91], v[74:75], v[84:85]
	v_pk_add_f32 v[74:75], v[74:75], v[84:85] neg_lo:[0,1] neg_hi:[0,1]
	s_nop 0
	v_xor_b32_e32 v84, 0x80000000, v75
	v_mov_b32_e32 v85, v74
	v_pk_add_f32 v[74:75], v[76:77], v[96:97]
	v_pk_add_f32 v[76:77], v[76:77], v[96:97] neg_lo:[0,1] neg_hi:[0,1]
	s_nop 0
	v_xor_b32_e32 v96, 0x80000000, v77
	v_mov_b32_e32 v97, v76
	v_pk_mul_f32 v[96:97], v[20:21], v[96:97] op_sel_hi:[0,1]
	v_pk_fma_f32 v[76:77], v[50:51], v[76:77], v[96:97] op_sel_hi:[0,1,1] neg_lo:[1,0,0] neg_hi:[1,0,0]
	v_pk_add_f32 v[96:97], v[78:79], v[94:95]
	v_pk_add_f32 v[78:79], v[78:79], v[94:95] neg_lo:[0,1] neg_hi:[0,1]
	s_nop 0
	v_xor_b32_e32 v94, 0x80000000, v79
	v_mov_b32_e32 v95, v78
	v_pk_mul_f32 v[94:95], v[10:11], v[94:95] op_sel_hi:[0,1]
	v_pk_fma_f32 v[78:79], v[10:11], v[78:79], v[94:95] op_sel_hi:[0,1,1] neg_lo:[1,0,0] neg_hi:[1,0,0]
	v_pk_add_f32 v[94:95], v[80:81], v[66:67]
	v_pk_add_f32 v[66:67], v[80:81], v[66:67] neg_lo:[0,1] neg_hi:[0,1]
	s_nop 0
	v_xor_b32_e32 v80, 0x80000000, v67
	v_mov_b32_e32 v81, v66
	v_pk_mul_f32 v[80:81], v[50:51], v[80:81] op_sel_hi:[0,1]
	v_pk_fma_f32 v[66:67], v[20:21], v[66:67], v[80:81] op_sel_hi:[0,1,1] neg_lo:[1,0,0] neg_hi:[1,0,0]
	v_pk_add_f32 v[80:81], v[68:69], v[90:91]
	v_pk_add_f32 v[68:69], v[68:69], v[90:91] neg_lo:[0,1] neg_hi:[0,1]
	v_pk_add_f32 v[90:91], v[92:93], v[74:75]
	v_pk_add_f32 v[74:75], v[92:93], v[74:75] neg_lo:[0,1] neg_hi:[0,1]
	s_nop 0
	v_xor_b32_e32 v92, 0x80000000, v75
	v_mov_b32_e32 v93, v74
	v_pk_mul_f32 v[92:93], v[10:11], v[92:93] op_sel_hi:[0,1]
	v_pk_fma_f32 v[74:75], v[10:11], v[74:75], v[92:93] op_sel_hi:[0,1,1]
	v_pk_add_f32 v[92:93], v[52:53], v[96:97]
	v_pk_add_f32 v[52:53], v[52:53], v[96:97] neg_lo:[0,1] neg_hi:[0,1]
	s_nop 0
	v_xor_b32_e32 v96, 0x80000000, v53
	v_mov_b32_e32 v97, v52
	v_pk_add_f32 v[52:53], v[88:89], v[94:95]
	v_pk_add_f32 v[88:89], v[88:89], v[94:95] neg_lo:[0,1] neg_hi:[0,1]
	s_nop 0
	v_xor_b32_e32 v94, 0x80000000, v89
	v_mov_b32_e32 v95, v88
	v_pk_mul_f32 v[94:95], v[10:11], v[94:95] op_sel_hi:[0,1]
	v_pk_fma_f32 v[88:89], v[10:11], v[88:89], v[94:95] op_sel_hi:[0,1,1] neg_lo:[1,0,0] neg_hi:[1,0,0]
	v_pk_add_f32 v[94:95], v[80:81], v[92:93]
	v_pk_add_f32 v[80:81], v[80:81], v[92:93] neg_lo:[0,1] neg_hi:[0,1]
	v_pk_add_f32 v[92:93], v[90:91], v[52:53]
	v_pk_add_f32 v[52:53], v[90:91], v[52:53] neg_lo:[0,1] neg_hi:[0,1]
	s_nop 0
	v_xor_b32_e32 v90, 0x80000000, v53
	v_mov_b32_e32 v91, v52
	v_pk_add_f32 v[52:53], v[94:95], v[92:93]
	v_pk_add_f32 v[92:93], v[94:95], v[92:93] neg_lo:[0,1] neg_hi:[0,1]
	v_pk_add_f32 v[94:95], v[80:81], v[90:91]
	v_pk_add_f32 v[80:81], v[80:81], v[90:91] neg_lo:[0,1] neg_hi:[0,1]
	v_pk_add_f32 v[90:91], v[68:69], v[96:97]
	v_pk_add_f32 v[68:69], v[68:69], v[96:97] neg_lo:[0,1] neg_hi:[0,1]
	v_pk_add_f32 v[96:97], v[74:75], v[88:89]
	v_pk_add_f32 v[74:75], v[74:75], v[88:89] neg_lo:[0,1] neg_hi:[0,1]
	s_nop 0
	v_xor_b32_e32 v88, 0x80000000, v75
	v_mov_b32_e32 v89, v74
	v_pk_add_f32 v[74:75], v[90:91], v[96:97]
	v_pk_add_f32 v[90:91], v[90:91], v[96:97] neg_lo:[0,1] neg_hi:[0,1]
	v_pk_add_f32 v[96:97], v[68:69], v[88:89]
	v_pk_add_f32 v[68:69], v[68:69], v[88:89] neg_lo:[0,1] neg_hi:[0,1]
	v_pk_add_f32 v[88:89], v[82:83], v[84:85]
	v_pk_add_f32 v[82:83], v[82:83], v[84:85] neg_lo:[0,1] neg_hi:[0,1]
	v_pk_add_f32 v[84:85], v[34:35], v[76:77]
	v_pk_add_f32 v[34:35], v[34:35], v[76:77] neg_lo:[0,1] neg_hi:[0,1]
	s_nop 0
	v_xor_b32_e32 v76, 0x80000000, v35
	v_mov_b32_e32 v77, v34
	v_pk_mul_f32 v[76:77], v[10:11], v[76:77] op_sel_hi:[0,1]
	v_pk_fma_f32 v[34:35], v[10:11], v[34:35], v[76:77] op_sel_hi:[0,1,1]
	v_pk_add_f32 v[76:77], v[70:71], v[78:79]
	v_pk_add_f32 v[70:71], v[70:71], v[78:79] neg_lo:[0,1] neg_hi:[0,1]
	s_nop 0
	v_xor_b32_e32 v78, 0x80000000, v71
	v_mov_b32_e32 v79, v70
	v_pk_add_f32 v[70:71], v[72:73], v[66:67]
	v_pk_add_f32 v[66:67], v[72:73], v[66:67] neg_lo:[0,1] neg_hi:[0,1]
	s_nop 0
	v_xor_b32_e32 v72, 0x80000000, v67
	v_mov_b32_e32 v73, v66
	v_pk_mul_f32 v[72:73], v[10:11], v[72:73] op_sel_hi:[0,1]
	v_pk_fma_f32 v[66:67], v[10:11], v[66:67], v[72:73] op_sel_hi:[0,1,1] neg_lo:[1,0,0] neg_hi:[1,0,0]
	v_pk_add_f32 v[72:73], v[88:89], v[76:77]
	v_pk_add_f32 v[76:77], v[88:89], v[76:77] neg_lo:[0,1] neg_hi:[0,1]
	v_pk_add_f32 v[88:89], v[84:85], v[70:71]
	v_pk_add_f32 v[70:71], v[84:85], v[70:71] neg_lo:[0,1] neg_hi:[0,1]
	s_nop 0
	v_xor_b32_e32 v84, 0x80000000, v71
	v_mov_b32_e32 v85, v70
	v_pk_add_f32 v[70:71], v[72:73], v[88:89]
	v_pk_add_f32 v[72:73], v[72:73], v[88:89] neg_lo:[0,1] neg_hi:[0,1]
	v_pk_add_f32 v[88:89], v[76:77], v[84:85]
	v_pk_add_f32 v[76:77], v[76:77], v[84:85] neg_lo:[0,1] neg_hi:[0,1]
	v_pk_add_f32 v[84:85], v[82:83], v[78:79]
	v_pk_add_f32 v[78:79], v[82:83], v[78:79] neg_lo:[0,1] neg_hi:[0,1]
	v_pk_add_f32 v[82:83], v[34:35], v[66:67]
	v_pk_add_f32 v[34:35], v[34:35], v[66:67] neg_lo:[0,1] neg_hi:[0,1]
	s_nop 0
	v_xor_b32_e32 v66, 0x80000000, v35
	v_mov_b32_e32 v67, v34
	v_pk_add_f32 v[34:35], v[84:85], v[82:83]
	v_pk_add_f32 v[82:83], v[84:85], v[82:83] neg_lo:[0,1] neg_hi:[0,1]
	v_pk_add_f32 v[84:85], v[78:79], v[66:67]
	v_pk_add_f32 v[66:67], v[78:79], v[66:67] neg_lo:[0,1] neg_hi:[0,1]
	v_pk_add_f32 v[78:79], v[16:17], v[86:87]
	v_pk_add_f32 v[16:17], v[16:17], v[86:87] neg_lo:[0,1] neg_hi:[0,1]
	v_pk_add_f32 v[86:87], v[18:19], v[36:37]
	v_pk_add_f32 v[18:19], v[18:19], v[36:37] neg_lo:[0,1] neg_hi:[0,1]
	s_nop 0
	v_xor_b32_e32 v36, 0x80000000, v19
	v_mov_b32_e32 v37, v18
	v_pk_mul_f32 v[36:37], v[50:51], v[36:37] op_sel_hi:[0,1]
	v_pk_fma_f32 v[18:19], v[20:21], v[18:19], v[36:37] op_sel_hi:[0,1,1]
	v_pk_add_f32 v[36:37], v[22:23], v[38:39]
	v_pk_add_f32 v[22:23], v[22:23], v[38:39] neg_lo:[0,1] neg_hi:[0,1]
	s_nop 0
	v_xor_b32_e32 v38, 0x80000000, v23
	v_mov_b32_e32 v39, v22
	v_pk_mul_f32 v[38:39], v[10:11], v[38:39] op_sel_hi:[0,1]
	v_pk_fma_f32 v[22:23], v[10:11], v[22:23], v[38:39] op_sel_hi:[0,1,1]
	v_pk_add_f32 v[38:39], v[24:25], v[40:41]
	v_pk_add_f32 v[24:25], v[24:25], v[40:41] neg_lo:[0,1] neg_hi:[0,1]
	s_nop 0
	v_xor_b32_e32 v40, 0x80000000, v25
	v_mov_b32_e32 v41, v24
	v_pk_mul_f32 v[40:41], v[20:21], v[40:41] op_sel_hi:[0,1]
	v_pk_fma_f32 v[24:25], v[50:51], v[24:25], v[40:41] op_sel_hi:[0,1,1]
	v_pk_add_f32 v[40:41], v[28:29], v[44:45]
	v_pk_add_f32 v[28:29], v[28:29], v[44:45] neg_lo:[0,1] neg_hi:[0,1]
	s_nop 0
	v_xor_b32_e32 v44, 0x80000000, v29
	v_mov_b32_e32 v45, v28
	v_pk_add_f32 v[28:29], v[26:27], v[42:43]
	v_pk_add_f32 v[26:27], v[26:27], v[42:43] neg_lo:[0,1] neg_hi:[0,1]
	s_nop 0
	v_xor_b32_e32 v42, 0x80000000, v27
	v_mov_b32_e32 v43, v26
	v_pk_mul_f32 v[42:43], v[20:21], v[42:43] op_sel_hi:[0,1]
	v_pk_fma_f32 v[26:27], v[50:51], v[26:27], v[42:43] op_sel_hi:[0,1,1] neg_lo:[1,0,0] neg_hi:[1,0,0]
	v_pk_add_f32 v[42:43], v[30:31], v[46:47]
	v_pk_add_f32 v[30:31], v[30:31], v[46:47] neg_lo:[0,1] neg_hi:[0,1]
	s_nop 0
	v_xor_b32_e32 v46, 0x80000000, v31
	v_mov_b32_e32 v47, v30
	v_pk_mul_f32 v[46:47], v[10:11], v[46:47] op_sel_hi:[0,1]
	v_pk_fma_f32 v[30:31], v[10:11], v[30:31], v[46:47] op_sel_hi:[0,1,1] neg_lo:[1,0,0] neg_hi:[1,0,0]
	v_pk_add_f32 v[46:47], v[32:33], v[48:49]
	v_pk_add_f32 v[32:33], v[32:33], v[48:49] neg_lo:[0,1] neg_hi:[0,1]
	s_nop 0
	v_xor_b32_e32 v48, 0x80000000, v33
	v_mov_b32_e32 v49, v32
	v_pk_mul_f32 v[48:49], v[50:51], v[48:49] op_sel_hi:[0,1]
	v_pk_fma_f32 v[20:21], v[20:21], v[32:33], v[48:49] op_sel_hi:[0,1,1] neg_lo:[1,0,0] neg_hi:[1,0,0]
	v_pk_add_f32 v[48:49], v[86:87], v[28:29]
	v_pk_add_f32 v[28:29], v[86:87], v[28:29] neg_lo:[0,1] neg_hi:[0,1]
	v_pk_add_f32 v[32:33], v[78:79], v[40:41]
	v_pk_add_f32 v[40:41], v[78:79], v[40:41] neg_lo:[0,1] neg_hi:[0,1]
	v_xor_b32_e32 v78, 0x80000000, v29
	v_mov_b32_e32 v79, v28
	v_pk_mul_f32 v[78:79], v[10:11], v[78:79] op_sel_hi:[0,1]
	v_pk_fma_f32 v[28:29], v[10:11], v[28:29], v[78:79] op_sel_hi:[0,1,1]
	v_pk_add_f32 v[78:79], v[36:37], v[42:43]
	v_pk_add_f32 v[36:37], v[36:37], v[42:43] neg_lo:[0,1] neg_hi:[0,1]
	s_nop 0
	v_xor_b32_e32 v42, 0x80000000, v37
	v_mov_b32_e32 v43, v36
	v_pk_add_f32 v[36:37], v[38:39], v[46:47]
	v_pk_add_f32 v[38:39], v[38:39], v[46:47] neg_lo:[0,1] neg_hi:[0,1]
	s_nop 0
	v_xor_b32_e32 v46, 0x80000000, v39
	v_mov_b32_e32 v47, v38
	v_pk_mul_f32 v[46:47], v[10:11], v[46:47] op_sel_hi:[0,1]
	v_pk_fma_f32 v[38:39], v[10:11], v[38:39], v[46:47] op_sel_hi:[0,1,1] neg_lo:[1,0,0] neg_hi:[1,0,0]
	v_pk_add_f32 v[46:47], v[32:33], v[78:79]
	v_pk_add_f32 v[32:33], v[32:33], v[78:79] neg_lo:[0,1] neg_hi:[0,1]
	v_pk_add_f32 v[78:79], v[48:49], v[36:37]
	v_pk_add_f32 v[36:37], v[48:49], v[36:37] neg_lo:[0,1] neg_hi:[0,1]
	s_nop 0
	v_xor_b32_e32 v48, 0x80000000, v37
	v_mov_b32_e32 v49, v36
	v_pk_add_f32 v[86:87], v[32:33], v[48:49]
	v_pk_add_f32 v[32:33], v[32:33], v[48:49] neg_lo:[0,1] neg_hi:[0,1]
	v_pk_add_f32 v[48:49], v[40:41], v[42:43]
	v_pk_add_f32 v[40:41], v[40:41], v[42:43] neg_lo:[0,1] neg_hi:[0,1]
	v_pk_add_f32 v[42:43], v[28:29], v[38:39]
	v_pk_add_f32 v[28:29], v[28:29], v[38:39] neg_lo:[0,1] neg_hi:[0,1]
	v_pk_add_f32 v[36:37], v[46:47], v[78:79] neg_lo:[0,1] neg_hi:[0,1]
	v_xor_b32_e32 v38, 0x80000000, v29
	v_mov_b32_e32 v39, v28
	v_pk_add_f32 v[28:29], v[48:49], v[42:43]
	v_pk_add_f32 v[42:43], v[48:49], v[42:43] neg_lo:[0,1] neg_hi:[0,1]
	v_pk_add_f32 v[48:49], v[40:41], v[38:39]
	v_pk_add_f32 v[38:39], v[40:41], v[38:39] neg_lo:[0,1] neg_hi:[0,1]
	v_pk_add_f32 v[40:41], v[16:17], v[44:45]
	v_pk_add_f32 v[16:17], v[16:17], v[44:45] neg_lo:[0,1] neg_hi:[0,1]
	v_pk_add_f32 v[44:45], v[18:19], v[26:27]
	v_pk_add_f32 v[18:19], v[18:19], v[26:27] neg_lo:[0,1] neg_hi:[0,1]
	s_nop 0
	v_xor_b32_e32 v26, 0x80000000, v19
	v_mov_b32_e32 v27, v18
	v_pk_mul_f32 v[26:27], v[10:11], v[26:27] op_sel_hi:[0,1]
	v_pk_fma_f32 v[18:19], v[10:11], v[18:19], v[26:27] op_sel_hi:[0,1,1]
	v_pk_add_f32 v[26:27], v[22:23], v[30:31]
	v_pk_add_f32 v[22:23], v[22:23], v[30:31] neg_lo:[0,1] neg_hi:[0,1]
	s_nop 0
	v_xor_b32_e32 v30, 0x80000000, v23
	v_mov_b32_e32 v31, v22
	v_pk_add_f32 v[22:23], v[24:25], v[20:21]
	v_pk_add_f32 v[20:21], v[24:25], v[20:21] neg_lo:[0,1] neg_hi:[0,1]
	s_nop 0
	v_xor_b32_e32 v24, 0x80000000, v21
	v_mov_b32_e32 v25, v20
	v_pk_mul_f32 v[24:25], v[10:11], v[24:25] op_sel_hi:[0,1]
	v_pk_fma_f32 v[20:21], v[10:11], v[20:21], v[24:25] op_sel_hi:[0,1,1] neg_lo:[1,0,0] neg_hi:[1,0,0]
	v_pk_add_f32 v[24:25], v[40:41], v[26:27]
	v_pk_add_f32 v[26:27], v[40:41], v[26:27] neg_lo:[0,1] neg_hi:[0,1]
	v_pk_add_f32 v[40:41], v[44:45], v[22:23]
	v_pk_add_f32 v[22:23], v[44:45], v[22:23] neg_lo:[0,1] neg_hi:[0,1]
	s_nop 0
	v_xor_b32_e32 v44, 0x80000000, v23
	v_mov_b32_e32 v45, v22
	v_pk_add_f32 v[22:23], v[24:25], v[40:41]
	v_pk_add_f32 v[24:25], v[24:25], v[40:41] neg_lo:[0,1] neg_hi:[0,1]
	v_pk_add_f32 v[40:41], v[26:27], v[44:45]
	v_pk_add_f32 v[26:27], v[26:27], v[44:45] neg_lo:[0,1] neg_hi:[0,1]
	v_pk_add_f32 v[44:45], v[16:17], v[30:31]
	v_pk_add_f32 v[16:17], v[16:17], v[30:31] neg_lo:[0,1] neg_hi:[0,1]
	v_pk_add_f32 v[30:31], v[18:19], v[20:21]
	v_pk_add_f32 v[18:19], v[18:19], v[20:21] neg_lo:[0,1] neg_hi:[0,1]
	s_nop 0
	v_xor_b32_e32 v20, 0x80000000, v19
	v_mov_b32_e32 v21, v18
	v_pk_add_f32 v[18:19], v[44:45], v[30:31]
	v_pk_add_f32 v[30:31], v[44:45], v[30:31] neg_lo:[0,1] neg_hi:[0,1]
	v_pk_add_f32 v[44:45], v[16:17], v[20:21]
	v_pk_add_f32 v[16:17], v[16:17], v[20:21] neg_lo:[0,1] neg_hi:[0,1]
	v_pk_add_f32 v[20:21], v[46:47], v[78:79]
	ds_write2_b64 v13, v[52:53], v[20:21] offset1:16
	ds_write2_b64 v15, v[70:71], v[22:23] offset0:32 offset1:48
	ds_write2_b64 v51, v[74:75], v[28:29] offset0:64 offset1:80
	ds_write2_b64 v54, v[34:35], v[18:19] offset0:96 offset1:112
	ds_write2_b64 v55, v[94:95], v[86:87] offset0:128 offset1:144
	ds_write2_b64 v56, v[88:89], v[40:41] offset0:160 offset1:176
	ds_write2_b64 v57, v[96:97], v[48:49] offset0:192 offset1:208
	ds_write2_b64 v58, v[84:85], v[44:45] offset0:224 offset1:240
	ds_write2_b64 v59, v[92:93], v[36:37] offset1:16
	ds_write2_b64 v60, v[72:73], v[24:25] offset0:32 offset1:48
	ds_write2_b64 v61, v[90:91], v[42:43] offset0:64 offset1:80
	ds_write2_b64 v62, v[82:83], v[30:31] offset0:96 offset1:112
	ds_write2_b64 v63, v[80:81], v[32:33] offset0:128 offset1:144
	ds_write2_b64 v64, v[76:77], v[26:27] offset0:160 offset1:176
	ds_write2_b64 v65, v[68:69], v[38:39] offset0:192 offset1:208
	ds_write2_b64 v101, v[66:67], v[16:17] offset0:224 offset1:240
	v_mov_b32_e32 v10, v174
	s_waitcnt lgkmcnt(0)
	s_barrier
	v_mov_b32_e32 v22, v180
	v_mov_b32_e32 v23, v181
	v_lshl_add_u32 v10, v10, 3, 0
	ds_read_b64 v[16:17], v10
	ds_read_b64 v[80:81], v10 offset:4224
	ds_read_b64 v[78:79], v10 offset:8448
	ds_read_b64 v[76:77], v10 offset:12672
	ds_read_b64 v[74:75], v10 offset:16896
	ds_read_b64 v[72:73], v10 offset:21120
	ds_read_b64 v[70:71], v10 offset:25344
	ds_read_b64 v[68:69], v10 offset:29568
	ds_read_b64 v[24:25], v10 offset:33792
	ds_read_b64 v[62:63], v10 offset:38016
	ds_read_b64 v[60:61], v10 offset:42240
	ds_read_b64 v[58:59], v10 offset:46464
	ds_read_b64 v[54:55], v10 offset:50688
	ds_read_b64 v[50:51], v10 offset:54912
	ds_read_b64 v[46:47], v10 offset:59136
	ds_read_b64 v[44:45], v10 offset:63360
	v_add_u32_e32 v13, 0x10800, v10
	v_add_u32_e32 v15, 0x11880, v10
	v_add_u32_e32 v20, 0x12900, v10
	v_add_u32_e32 v21, 0x13980, v10
	ds_read_b64 v[18:19], v13
	ds_read_b64 v[66:67], v15
	ds_read_b64 v[64:65], v20
	ds_read_b64 v[38:39], v21
	v_add_u32_e32 v13, 0x14a00, v10
	v_add_u32_e32 v15, 0x15a80, v10
	v_add_u32_e32 v20, 0x16b00, v10
	v_add_u32_e32 v21, 0x17b80, v10
	ds_read_b64 v[30:31], v13
	ds_read_b64 v[56:57], v15
	ds_read_b64 v[52:53], v20
	ds_read_b64 v[48:49], v21
	v_add_u32_e32 v13, 0x18c00, v10
	v_add_u32_e32 v15, 0x19c80, v10
	v_add_u32_e32 v20, 0x1ad00, v10
	v_add_u32_e32 v21, 0x1bd80, v10
	ds_read_b64 v[82:83], v13
	ds_read_b64 v[42:43], v15
	ds_read_b64 v[40:41], v20
	ds_read_b64 v[36:37], v21
	v_add_u32_e32 v13, 0x1ce00, v10
	v_add_u32_e32 v15, 0x1de80, v10
	v_add_u32_e32 v20, 0x1ef00, v10
	v_add_u32_e32 v10, 0x1ff80, v10
	ds_read_b64 v[34:35], v13
	ds_read_b64 v[32:33], v15
	ds_read_b64 v[28:29], v20
	ds_read_b64 v[26:27], v10
	v_pk_fma_f32 v[84:85], v[22:23], s[92:93], v[22:23] op_sel:[1,0,0] op_sel_hi:[0,1,1]
	v_xor_b32_e32 v20, 0x80000000, v85
	v_mov_b32_e32 v21, v85
	v_pk_mul_f32 v[20:21], v[22:23], v[20:21] op_sel:[1,0] op_sel_hi:[0,1]
	v_pk_fma_f32 v[86:87], v[22:23], v[84:85], v[20:21] op_sel_hi:[1,0,1]
	v_mov_b32_e32 v10, v164
	v_xor_b32_e32 v20, 0x80000000, v87
	v_mov_b32_e32 v21, v87
	v_pk_mul_f32 v[20:21], v[22:23], v[20:21] op_sel:[1,0] op_sel_hi:[0,1]
	v_pk_fma_f32 v[88:89], v[22:23], v[86:87], v[20:21] op_sel_hi:[1,0,1]
	s_waitcnt lgkmcnt(14)
	v_fmac_f32_e32 v16, 0, v17
	v_xor_b32_e32 v20, 0x80000000, v89
	v_mov_b32_e32 v21, v89
	v_pk_mul_f32 v[20:21], v[22:23], v[20:21] op_sel:[1,0] op_sel_hi:[0,1]
	v_pk_fma_f32 v[90:91], v[22:23], v[88:89], v[20:21] op_sel_hi:[1,0,1]
	v_mov_b32_e32 v10, v165
	v_xor_b32_e32 v20, 0x80000000, v91
	v_mov_b32_e32 v21, v91
	v_pk_mul_f32 v[20:21], v[22:23], v[20:21] op_sel:[1,0] op_sel_hi:[0,1]
	v_pk_fma_f32 v[92:93], v[22:23], v[90:91], v[20:21] op_sel_hi:[1,0,1]
	v_mov_b32_e32 v13, v172
	v_xor_b32_e32 v20, 0x80000000, v93
	v_mov_b32_e32 v21, v93
	v_pk_mul_f32 v[20:21], v[22:23], v[20:21] op_sel:[1,0] op_sel_hi:[0,1]
	v_pk_fma_f32 v[94:95], v[22:23], v[92:93], v[20:21] op_sel_hi:[1,0,1]
	v_readlane_b32 s72, v251, 48
	v_xor_b32_e32 v20, 0x80000000, v95
	v_mov_b32_e32 v21, v95
	v_pk_mul_f32 v[20:21], v[22:23], v[20:21] op_sel:[1,0] op_sel_hi:[0,1]
	v_pk_fma_f32 v[96:97], v[22:23], v[94:95], v[20:21] op_sel_hi:[1,0,1]
	v_readlane_b32 s73, v251, 49
	v_xor_b32_e32 v20, 0x80000000, v97
	v_mov_b32_e32 v21, v97
	v_pk_mul_f32 v[20:21], v[22:23], v[20:21] op_sel:[1,0] op_sel_hi:[0,1]
	v_pk_fma_f32 v[98:99], v[22:23], v[96:97], v[20:21] op_sel_hi:[1,0,1]
	s_movk_i32 s10, 0xda00
	v_xor_b32_e32 v20, 0x80000000, v99
	v_mov_b32_e32 v21, v99
	v_pk_mul_f32 v[20:21], v[22:23], v[20:21] op_sel:[1,0] op_sel_hi:[0,1]
	v_pk_fma_f32 v[100:101], v[22:23], v[98:99], v[20:21] op_sel_hi:[1,0,1]
	s_mov_b32 s20, 0x3f61c598
	v_xor_b32_e32 v20, 0x80000000, v101
	v_mov_b32_e32 v21, v101
	v_pk_mul_f32 v[20:21], v[22:23], v[20:21] op_sel:[1,0] op_sel_hi:[0,1]
	v_pk_fma_f32 v[102:103], v[22:23], v[100:101], v[20:21] op_sel_hi:[1,0,1]
	s_mov_b32 s52, s95
	v_xor_b32_e32 v20, 0x80000000, v103
	v_mov_b32_e32 v21, v103
	v_pk_mul_f32 v[20:21], v[22:23], v[20:21] op_sel:[1,0] op_sel_hi:[0,1]
	v_pk_fma_f32 v[104:105], v[22:23], v[102:103], v[20:21] op_sel_hi:[1,0,1]
	s_mov_b32 s53, s94
	v_xor_b32_e32 v20, 0x80000000, v105
	v_mov_b32_e32 v21, v105
	v_pk_mul_f32 v[20:21], v[22:23], v[20:21] op_sel:[1,0] op_sel_hi:[0,1]
	v_pk_fma_f32 v[106:107], v[22:23], v[104:105], v[20:21] op_sel_hi:[1,0,1]
	s_mov_b32 s21, 0xbef15aea
	v_xor_b32_e32 v20, 0x80000000, v107
	v_mov_b32_e32 v21, v107
	v_pk_mul_f32 v[20:21], v[22:23], v[20:21] op_sel:[1,0] op_sel_hi:[0,1]
	v_pk_fma_f32 v[108:109], v[22:23], v[106:107], v[20:21] op_sel_hi:[1,0,1]
	s_mov_b32 s40, s47
	v_xor_b32_e32 v20, 0x80000000, v109
	v_mov_b32_e32 v21, v109
	v_pk_mul_f32 v[20:21], v[22:23], v[20:21] op_sel:[1,0] op_sel_hi:[0,1]
	v_pk_fma_f32 v[110:111], v[22:23], v[108:109], v[20:21] op_sel_hi:[1,0,1]
	s_mov_b32 s41, s42
	v_xor_b32_e32 v20, 0x80000000, v111
	v_mov_b32_e32 v21, v111
	v_pk_mul_f32 v[20:21], v[22:23], v[20:21] op_sel:[1,0] op_sel_hi:[0,1]
	v_pk_fma_f32 v[112:113], v[22:23], v[110:111], v[20:21] op_sel_hi:[1,0,1]
	s_mov_b32 s38, 0x3f3504f3
	v_xor_b32_e32 v20, 0x80000000, v113
	v_mov_b32_e32 v21, v113
	v_pk_mul_f32 v[20:21], v[22:23], v[20:21] op_sel:[1,0] op_sel_hi:[0,1]
	v_pk_fma_f32 v[20:21], v[22:23], v[112:113], v[20:21] op_sel_hi:[1,0,1]
	s_mov_b32 s39, 0xbf3504f3
	v_xor_b32_e32 v114, 0x80000000, v21
	v_mov_b32_e32 v115, v21
	v_pk_mul_f32 v[114:115], v[22:23], v[114:115] op_sel:[1,0] op_sel_hi:[0,1]
	v_pk_fma_f32 v[114:115], v[22:23], v[20:21], v[114:115] op_sel_hi:[1,0,1]
	v_mul_f32_e32 v18, v18, v20
	v_xor_b32_e32 v116, 0x80000000, v115
	v_mov_b32_e32 v117, v115
	v_pk_mul_f32 v[116:117], v[22:23], v[116:117] op_sel:[1,0] op_sel_hi:[0,1]
	v_pk_fma_f32 v[116:117], v[22:23], v[114:115], v[116:117] op_sel_hi:[1,0,1]
	v_fmac_f32_e32 v18, v19, v21
	v_xor_b32_e32 v118, 0x80000000, v117
	v_mov_b32_e32 v119, v117
	v_pk_mul_f32 v[118:119], v[22:23], v[118:119] op_sel:[1,0] op_sel_hi:[0,1]
	v_pk_fma_f32 v[118:119], v[22:23], v[116:117], v[118:119] op_sel_hi:[1,0,1]
	v_add_f32_e32 v17, v16, v18
	v_xor_b32_e32 v120, 0x80000000, v119
	v_mov_b32_e32 v121, v119
	v_pk_mul_f32 v[120:121], v[22:23], v[120:121] op_sel:[1,0] op_sel_hi:[0,1]
	v_pk_fma_f32 v[120:121], v[22:23], v[118:119], v[120:121] op_sel_hi:[1,0,1]
	s_mov_b32 s28, 0x3f226799
	v_xor_b32_e32 v122, 0x80000000, v121
	v_mov_b32_e32 v123, v121
	v_pk_mul_f32 v[122:123], v[22:23], v[122:123] op_sel:[1,0] op_sel_hi:[0,1]
	v_pk_fma_f32 v[122:123], v[22:23], v[120:121], v[122:123] op_sel_hi:[1,0,1]
	s_mov_b32 s29, 0xbf45e403
	v_xor_b32_e32 v124, 0x80000000, v123
	v_mov_b32_e32 v125, v123
	v_pk_mul_f32 v[124:125], v[22:23], v[124:125] op_sel:[1,0] op_sel_hi:[0,1]
	v_pk_fma_f32 v[124:125], v[22:23], v[122:123], v[124:125] op_sel_hi:[1,0,1]
	s_mov_b32 s82, 0x3f0e39da
	v_xor_b32_e32 v126, 0x80000000, v125
	v_mov_b32_e32 v127, v125
	v_pk_mul_f32 v[126:127], v[22:23], v[126:127] op_sel:[1,0] op_sel_hi:[0,1]
	v_pk_fma_f32 v[126:127], v[22:23], v[124:125], v[126:127] op_sel_hi:[1,0,1]
	s_mov_b32 s83, 0xbf54db31
	v_xor_b32_e32 v128, 0x80000000, v127
	v_mov_b32_e32 v129, v127
	v_pk_mul_f32 v[128:129], v[22:23], v[128:129] op_sel:[1,0] op_sel_hi:[0,1]
	v_pk_fma_f32 v[128:129], v[22:23], v[126:127], v[128:129] op_sel_hi:[1,0,1]
	s_mov_b32 s22, 0x3ef15aea
	v_xor_b32_e32 v130, 0x80000000, v129
	v_mov_b32_e32 v131, v129
	v_pk_mul_f32 v[130:131], v[22:23], v[130:131] op_sel:[1,0] op_sel_hi:[0,1]
	v_pk_fma_f32 v[130:131], v[22:23], v[128:129], v[130:131] op_sel_hi:[1,0,1]
	s_mov_b32 s23, 0xbf61c598
	v_xor_b32_e32 v132, 0x80000000, v131
	v_mov_b32_e32 v133, v131
	v_pk_mul_f32 v[132:133], v[22:23], v[132:133] op_sel:[1,0] op_sel_hi:[0,1]
	v_pk_fma_f32 v[132:133], v[22:23], v[130:131], v[132:133] op_sel_hi:[1,0,1]
	s_mov_b32 s18, 0x3ec3ef15
	v_xor_b32_e32 v134, 0x80000000, v133
	v_mov_b32_e32 v135, v133
	v_pk_mul_f32 v[134:135], v[22:23], v[134:135] op_sel:[1,0] op_sel_hi:[0,1]
	v_pk_fma_f32 v[134:135], v[22:23], v[132:133], v[134:135] op_sel_hi:[1,0,1]
	s_mov_b32 s19, 0xbf6c835e
	v_xor_b32_e32 v136, 0x80000000, v135
	v_mov_b32_e32 v137, v135
	v_pk_mul_f32 v[136:137], v[22:23], v[136:137] op_sel:[1,0] op_sel_hi:[0,1]
	v_pk_fma_f32 v[136:137], v[22:23], v[134:135], v[136:137] op_sel_hi:[1,0,1]
	s_mov_b32 s24, 0x3f54db31
	v_xor_b32_e32 v138, 0x80000000, v137
	v_mov_b32_e32 v139, v137
	v_pk_mul_f32 v[138:139], v[22:23], v[138:139] op_sel:[1,0] op_sel_hi:[0,1]
	v_pk_fma_f32 v[138:139], v[22:23], v[136:137], v[138:139] op_sel_hi:[1,0,1]
	s_mov_b32 s25, 0xbf0e39da
	v_xor_b32_e32 v140, 0x80000000, v139
	v_mov_b32_e32 v141, v139
	v_pk_mul_f32 v[140:141], v[22:23], v[140:141] op_sel:[1,0] op_sel_hi:[0,1]
	v_pk_fma_f32 v[140:141], v[22:23], v[138:139], v[140:141] op_sel_hi:[1,0,1]
	s_mov_b32 s74, 0x3f45e403
	v_xor_b32_e32 v142, 0x80000000, v141
	v_mov_b32_e32 v143, v141
	v_pk_mul_f32 v[142:143], v[22:23], v[142:143] op_sel:[1,0] op_sel_hi:[0,1]
	v_pk_fma_f32 v[22:23], v[22:23], v[140:141], v[142:143] op_sel_hi:[1,0,1]
	s_waitcnt lgkmcnt(0)
	v_xor_b32_e32 v143, 0x80000000, v26
	v_mov_b32_e32 v142, v27
	v_pk_mul_f32 v[142:143], v[142:143], v[22:23] op_sel:[0,1]
	s_mov_b32 s75, 0xbf226799
	v_pk_fma_f32 v[26:27], v[26:27], v[22:23], v[142:143] op_sel_hi:[1,0,1]
	v_xor_b32_e32 v23, 0x80000000, v28
	v_mov_b32_e32 v22, v29
	v_pk_mul_f32 v[22:23], v[22:23], v[140:141] op_sel:[0,1]
	s_mov_b32 s36, s77
	v_pk_fma_f32 v[28:29], v[28:29], v[140:141], v[22:23] op_sel_hi:[1,0,1]
	v_xor_b32_e32 v23, 0x80000000, v32
	v_mov_b32_e32 v22, v33
	v_pk_mul_f32 v[22:23], v[22:23], v[138:139] op_sel:[0,1]
	s_mov_b32 s37, s43
	v_pk_fma_f32 v[32:33], v[32:33], v[138:139], v[22:23] op_sel_hi:[1,0,1]
	v_xor_b32_e32 v23, 0x80000000, v34
	v_mov_b32_e32 v22, v35
	v_pk_mul_f32 v[22:23], v[22:23], v[136:137] op_sel:[0,1]
	s_mov_b32 s76, s43
	v_pk_fma_f32 v[34:35], v[34:35], v[136:137], v[22:23] op_sel_hi:[1,0,1]
	v_xor_b32_e32 v23, 0x80000000, v36
	v_mov_b32_e32 v22, v37
	v_pk_mul_f32 v[22:23], v[22:23], v[134:135] op_sel:[0,1]
	s_mov_b32 s16, 0x3f6c835e
	v_pk_fma_f32 v[36:37], v[36:37], v[134:135], v[22:23] op_sel_hi:[1,0,1]
	v_xor_b32_e32 v23, 0x80000000, v40
	v_mov_b32_e32 v22, v41
	v_pk_mul_f32 v[22:23], v[22:23], v[132:133] op_sel:[0,1]
	s_mov_b32 s17, 0xbec3ef15
	v_pk_fma_f32 v[40:41], v[40:41], v[132:133], v[22:23] op_sel_hi:[1,0,1]
	v_xor_b32_e32 v23, 0x80000000, v42
	v_mov_b32_e32 v22, v43
	v_pk_mul_f32 v[22:23], v[22:23], v[130:131] op_sel:[0,1]
	s_mov_b32 s16, s19
	v_pk_fma_f32 v[42:43], v[42:43], v[130:131], v[22:23] op_sel_hi:[1,0,1]
	v_xor_b32_e32 v23, 0x80000000, v82
	v_mov_b32_e32 v22, v83
	v_pk_mul_f32 v[22:23], v[22:23], v[128:129] op_sel:[0,1]
	s_mov_b32 s27, s29
	v_pk_fma_f32 v[22:23], v[82:83], v[128:129], v[22:23] op_sel_hi:[1,0,1]
	v_xor_b32_e32 v83, 0x80000000, v48
	v_mov_b32_e32 v82, v49
	v_pk_mul_f32 v[82:83], v[82:83], v[126:127] op_sel:[0,1]
	s_mov_b32 s26, s75
	v_pk_fma_f32 v[48:49], v[48:49], v[126:127], v[82:83] op_sel_hi:[1,0,1]
	v_xor_b32_e32 v83, 0x80000000, v52
	v_mov_b32_e32 v82, v53
	v_pk_mul_f32 v[82:83], v[82:83], v[124:125] op_sel:[0,1]
	s_mov_b32 s46, s42
	v_pk_fma_f32 v[52:53], v[52:53], v[124:125], v[82:83] op_sel_hi:[1,0,1]
	v_xor_b32_e32 v83, 0x80000000, v56
	v_mov_b32_e32 v82, v57
	v_pk_mul_f32 v[82:83], v[82:83], v[122:123] op_sel:[0,1]
	v_mov_b32_e32 v124, v171
	v_pk_fma_f32 v[56:57], v[56:57], v[122:123], v[82:83] op_sel_hi:[1,0,1]
	v_xor_b32_e32 v83, 0x80000000, v30
	v_mov_b32_e32 v82, v31
	v_pk_mul_f32 v[82:83], v[82:83], v[120:121] op_sel:[0,1]
	v_mov_b32_e32 v122, v169
	v_pk_fma_f32 v[30:31], v[30:31], v[120:121], v[82:83] op_sel_hi:[1,0,1]
	v_xor_b32_e32 v83, 0x80000000, v38
	v_mov_b32_e32 v82, v39
	v_pk_mul_f32 v[82:83], v[82:83], v[118:119] op_sel:[0,1]
	v_mov_b32_e32 v120, v167
	v_pk_fma_f32 v[38:39], v[38:39], v[118:119], v[82:83] op_sel_hi:[1,0,1]
	v_xor_b32_e32 v83, 0x80000000, v64
	v_mov_b32_e32 v82, v65
	v_pk_mul_f32 v[82:83], v[82:83], v[116:117] op_sel:[0,1]
	v_mov_b32_e32 v118, v165
	v_pk_fma_f32 v[64:65], v[64:65], v[116:117], v[82:83] op_sel_hi:[1,0,1]
	v_xor_b32_e32 v83, 0x80000000, v66
	v_mov_b32_e32 v82, v67
	v_pk_mul_f32 v[82:83], v[82:83], v[114:115] op_sel:[0,1]
	s_nop 0
	v_pk_fma_f32 v[66:67], v[66:67], v[114:115], v[82:83] op_sel_hi:[1,0,1]
	v_xor_b32_e32 v83, 0x80000000, v44
	v_mov_b32_e32 v82, v45
	v_pk_mul_f32 v[82:83], v[82:83], v[112:113] op_sel:[0,1]
	s_nop 0
	v_pk_fma_f32 v[44:45], v[44:45], v[112:113], v[82:83] op_sel_hi:[1,0,1]
	v_xor_b32_e32 v83, 0x80000000, v46
	v_mov_b32_e32 v82, v47
	v_pk_mul_f32 v[82:83], v[82:83], v[110:111] op_sel:[0,1]
	s_nop 0
	v_pk_fma_f32 v[46:47], v[46:47], v[110:111], v[82:83] op_sel_hi:[1,0,1]
	v_xor_b32_e32 v83, 0x80000000, v50
	v_mov_b32_e32 v82, v51
	v_pk_mul_f32 v[82:83], v[82:83], v[108:109] op_sel:[0,1]
	s_nop 0
	v_pk_fma_f32 v[50:51], v[50:51], v[108:109], v[82:83] op_sel_hi:[1,0,1]
	v_xor_b32_e32 v83, 0x80000000, v54
	v_mov_b32_e32 v82, v55
	v_pk_mul_f32 v[82:83], v[82:83], v[106:107] op_sel:[0,1]
	s_nop 0
	v_pk_fma_f32 v[54:55], v[54:55], v[106:107], v[82:83] op_sel_hi:[1,0,1]
	v_xor_b32_e32 v83, 0x80000000, v58
	v_mov_b32_e32 v82, v59
	v_pk_mul_f32 v[82:83], v[82:83], v[104:105] op_sel:[0,1]
	s_nop 0
	v_pk_fma_f32 v[58:59], v[58:59], v[104:105], v[82:83] op_sel_hi:[1,0,1]
	v_xor_b32_e32 v83, 0x80000000, v60
	v_mov_b32_e32 v82, v61
	v_pk_mul_f32 v[82:83], v[82:83], v[102:103] op_sel:[0,1]
	s_nop 0
	v_pk_fma_f32 v[60:61], v[60:61], v[102:103], v[82:83] op_sel_hi:[1,0,1]
	v_xor_b32_e32 v83, 0x80000000, v62
	v_mov_b32_e32 v82, v63
	v_pk_mul_f32 v[82:83], v[82:83], v[100:101] op_sel:[0,1]
	s_nop 0
	v_pk_fma_f32 v[62:63], v[62:63], v[100:101], v[82:83] op_sel_hi:[1,0,1]
	v_xor_b32_e32 v83, 0x80000000, v24
	v_mov_b32_e32 v82, v25
	v_pk_mul_f32 v[82:83], v[82:83], v[98:99] op_sel:[0,1]
	s_nop 0
	v_pk_fma_f32 v[24:25], v[24:25], v[98:99], v[82:83] op_sel_hi:[1,0,1]
	v_xor_b32_e32 v83, 0x80000000, v68
	v_mov_b32_e32 v82, v69
	v_pk_mul_f32 v[82:83], v[82:83], v[96:97] op_sel:[0,1]
	v_add_f32_e32 v22, v24, v22
	v_pk_fma_f32 v[68:69], v[68:69], v[96:97], v[82:83] op_sel_hi:[1,0,1]
	v_xor_b32_e32 v83, 0x80000000, v70
	v_mov_b32_e32 v82, v71
	v_pk_mul_f32 v[82:83], v[82:83], v[94:95] op_sel:[0,1]
	v_add_f32_e32 v20, v17, v22
	v_pk_fma_f32 v[70:71], v[70:71], v[94:95], v[82:83] op_sel_hi:[1,0,1]
	v_xor_b32_e32 v83, 0x80000000, v72
	v_mov_b32_e32 v82, v73
	v_pk_mul_f32 v[82:83], v[82:83], v[92:93] op_sel:[0,1]
	v_mov_b32_e32 v94, v171
	v_pk_fma_f32 v[72:73], v[72:73], v[92:93], v[82:83] op_sel_hi:[1,0,1]
	v_xor_b32_e32 v83, 0x80000000, v74
	v_mov_b32_e32 v82, v75
	v_pk_mul_f32 v[82:83], v[82:83], v[90:91] op_sel:[0,1]
	v_mov_b32_e32 v92, v170
	v_pk_fma_f32 v[74:75], v[74:75], v[90:91], v[82:83] op_sel_hi:[1,0,1]
	v_xor_b32_e32 v83, 0x80000000, v76
	v_mov_b32_e32 v82, v77
	v_pk_mul_f32 v[82:83], v[82:83], v[88:89] op_sel:[0,1]
	v_mov_b32_e32 v90, v169
	v_pk_fma_f32 v[76:77], v[76:77], v[88:89], v[82:83] op_sel_hi:[1,0,1]
	v_xor_b32_e32 v83, 0x80000000, v78
	v_mov_b32_e32 v82, v79
	v_pk_mul_f32 v[82:83], v[82:83], v[86:87] op_sel:[0,1]
	v_mov_b32_e32 v88, v168
	v_pk_fma_f32 v[78:79], v[78:79], v[86:87], v[82:83] op_sel_hi:[1,0,1]
	v_xor_b32_e32 v83, 0x80000000, v80
	v_mov_b32_e32 v82, v81
	v_pk_mul_f32 v[82:83], v[84:85], v[82:83] op_sel:[1,0]
	v_mov_b32_e32 v86, v167
	v_pk_fma_f32 v[80:81], v[80:81], v[84:85], v[82:83] op_sel_hi:[1,0,1]
	v_mov_b32_e32 v84, v166
	v_pk_add_f32 v[96:97], v[80:81], v[66:67]
	v_pk_add_f32 v[66:67], v[80:81], v[66:67] neg_lo:[0,1] neg_hi:[0,1]
	s_nop 0
	v_xor_b32_e32 v80, 0x80000000, v67
	v_mov_b32_e32 v81, v66
	v_sub_f32_e32 v82, v25, v23
	v_pk_mul_f32 v[80:81], v[94:95], v[80:81] op_sel_hi:[0,1]
	v_pk_fma_f32 v[80:81], v[10:11], v[66:67], v[80:81] op_sel_hi:[0,1,1]
	v_pk_add_f32 v[66:67], v[78:79], v[64:65]
	v_pk_add_f32 v[64:65], v[78:79], v[64:65] neg_lo:[0,1] neg_hi:[0,1]
	s_nop 0
	v_xor_b32_e32 v78, 0x80000000, v65
	v_mov_b32_e32 v79, v64
	v_pk_mul_f32 v[78:79], v[92:93], v[78:79] op_sel_hi:[0,1]
	v_pk_fma_f32 v[64:65], v[84:85], v[64:65], v[78:79] op_sel_hi:[0,1,1]
	v_pk_add_f32 v[78:79], v[76:77], v[38:39]
	v_pk_add_f32 v[38:39], v[76:77], v[38:39] neg_lo:[0,1] neg_hi:[0,1]
	s_barrier
	v_xor_b32_e32 v76, 0x80000000, v39
	v_mov_b32_e32 v77, v38
	v_pk_mul_f32 v[76:77], v[90:91], v[76:77] op_sel_hi:[0,1]
	v_pk_fma_f32 v[76:77], v[86:87], v[38:39], v[76:77] op_sel_hi:[0,1,1]
	v_pk_add_f32 v[38:39], v[74:75], v[30:31]
	v_pk_add_f32 v[30:31], v[74:75], v[30:31] neg_lo:[0,1] neg_hi:[0,1]
	s_nop 0
	v_xor_b32_e32 v74, 0x80000000, v31
	v_mov_b32_e32 v75, v30
	v_pk_mul_f32 v[74:75], v[88:89], v[74:75] op_sel_hi:[0,1]
	v_pk_fma_f32 v[30:31], v[88:89], v[30:31], v[74:75] op_sel_hi:[0,1,1]
	v_pk_add_f32 v[74:75], v[72:73], v[56:57]
	v_pk_add_f32 v[56:57], v[72:73], v[56:57] neg_lo:[0,1] neg_hi:[0,1]
	v_sub_f32_e32 v22, v17, v22
	v_xor_b32_e32 v72, 0x80000000, v57
	v_mov_b32_e32 v73, v56
	v_pk_mul_f32 v[72:73], v[86:87], v[72:73] op_sel_hi:[0,1]
	v_pk_fma_f32 v[72:73], v[90:91], v[56:57], v[72:73] op_sel_hi:[0,1,1]
	v_pk_add_f32 v[56:57], v[70:71], v[52:53]
	v_pk_add_f32 v[52:53], v[70:71], v[52:53] neg_lo:[0,1] neg_hi:[0,1]
	v_ashrrev_i32_e32 v15, 31, v14
	v_xor_b32_e32 v70, 0x80000000, v53
	v_mov_b32_e32 v71, v52
	v_pk_mul_f32 v[70:71], v[84:85], v[70:71] op_sel_hi:[0,1]
	v_pk_fma_f32 v[52:53], v[92:93], v[52:53], v[70:71] op_sel_hi:[0,1,1]
	v_pk_add_f32 v[70:71], v[68:69], v[48:49]
	v_pk_add_f32 v[48:49], v[68:69], v[48:49] neg_lo:[0,1] neg_hi:[0,1]
	v_lshl_add_u64 v[14:15], v[14:15], 2, s[72:73]
	v_xor_b32_e32 v68, 0x80000000, v49
	v_mov_b32_e32 v69, v48
	v_pk_mul_f32 v[68:69], v[10:11], v[68:69] op_sel_hi:[0,1]
	v_pk_fma_f32 v[98:99], v[94:95], v[48:49], v[68:69] op_sel_hi:[0,1,1]
	v_pk_add_f32 v[48:49], v[62:63], v[42:43]
	v_pk_add_f32 v[42:43], v[62:63], v[42:43] neg_lo:[0,1] neg_hi:[0,1]
	v_pk_add_f32 v[68:69], v[58:59], v[36:37]
	v_xor_b32_e32 v62, 0x80000000, v43
	v_mov_b32_e32 v63, v42
	v_pk_mul_f32 v[62:63], v[10:11], v[62:63] op_sel_hi:[0,1]
	v_pk_fma_f32 v[62:63], v[94:95], v[42:43], v[62:63] op_sel_hi:[0,1,1] neg_lo:[1,0,0] neg_hi:[1,0,0]
	v_pk_add_f32 v[42:43], v[60:61], v[40:41]
	v_pk_add_f32 v[40:41], v[60:61], v[40:41] neg_lo:[0,1] neg_hi:[0,1]
	v_pk_add_f32 v[36:37], v[58:59], v[36:37] neg_lo:[0,1] neg_hi:[0,1]
	v_xor_b32_e32 v60, 0x80000000, v41
	v_mov_b32_e32 v61, v40
	v_pk_mul_f32 v[60:61], v[84:85], v[60:61] op_sel_hi:[0,1]
	v_pk_fma_f32 v[60:61], v[92:93], v[40:41], v[60:61] op_sel_hi:[0,1,1] neg_lo:[1,0,0] neg_hi:[1,0,0]
	v_xor_b32_e32 v40, 0x80000000, v37
	v_mov_b32_e32 v41, v36
	v_pk_mul_f32 v[40:41], v[86:87], v[40:41] op_sel_hi:[0,1]
	v_pk_fma_f32 v[100:101], v[90:91], v[36:37], v[40:41] op_sel_hi:[0,1,1] neg_lo:[1,0,0] neg_hi:[1,0,0]
	v_pk_add_f32 v[40:41], v[54:55], v[34:35]
	v_pk_add_f32 v[34:35], v[54:55], v[34:35] neg_lo:[0,1] neg_hi:[0,1]
	v_add_f32_e32 v38, v38, v40
	v_xor_b32_e32 v36, 0x80000000, v35
	v_mov_b32_e32 v37, v34
	v_pk_mul_f32 v[36:37], v[88:89], v[36:37] op_sel_hi:[0,1]
	v_pk_fma_f32 v[34:35], v[88:89], v[34:35], v[36:37] op_sel_hi:[0,1,1] neg_lo:[1,0,0] neg_hi:[1,0,0]
	v_pk_add_f32 v[36:37], v[50:51], v[32:33]
	v_pk_add_f32 v[32:33], v[50:51], v[32:33] neg_lo:[0,1] neg_hi:[0,1]
	v_add_f32_e32 v30, v30, v34
	v_xor_b32_e32 v50, 0x80000000, v33
	v_mov_b32_e32 v51, v32
	v_pk_mul_f32 v[50:51], v[90:91], v[50:51] op_sel_hi:[0,1]
	v_pk_fma_f32 v[86:87], v[86:87], v[32:33], v[50:51] op_sel_hi:[0,1,1] neg_lo:[1,0,0] neg_hi:[1,0,0]
	v_pk_add_f32 v[32:33], v[46:47], v[28:29]
	v_pk_add_f32 v[28:29], v[46:47], v[28:29] neg_lo:[0,1] neg_hi:[0,1]
	v_pk_add_f32 v[50:51], v[44:45], v[26:27]
	v_xor_b32_e32 v46, 0x80000000, v29
	v_mov_b32_e32 v47, v28
	v_pk_mul_f32 v[46:47], v[92:93], v[46:47] op_sel_hi:[0,1]
	v_pk_add_f32 v[26:27], v[44:45], v[26:27] neg_lo:[0,1] neg_hi:[0,1]
	v_pk_fma_f32 v[46:47], v[84:85], v[28:29], v[46:47] op_sel_hi:[0,1,1] neg_lo:[1,0,0] neg_hi:[1,0,0]
	v_xor_b32_e32 v28, 0x80000000, v27
	v_mov_b32_e32 v29, v26
	v_pk_mul_f32 v[28:29], v[94:95], v[28:29] op_sel_hi:[0,1]
	v_pk_fma_f32 v[90:91], v[10:11], v[26:27], v[28:29] op_sel_hi:[0,1,1] neg_lo:[1,0,0] neg_hi:[1,0,0]
	v_pk_add_f32 v[28:29], v[96:97], v[48:49] neg_lo:[0,1] neg_hi:[0,1]
	v_pk_add_f32 v[26:27], v[96:97], v[48:49]
	v_xor_b32_e32 v44, 0x80000000, v29
	v_mov_b32_e32 v45, v28
	v_pk_mul_f32 v[44:45], v[92:93], v[44:45] op_sel_hi:[0,1]
	v_pk_fma_f32 v[94:95], v[84:85], v[28:29], v[44:45] op_sel_hi:[0,1,1]
	v_pk_add_f32 v[28:29], v[66:67], v[42:43] neg_lo:[0,1] neg_hi:[0,1]
	v_pk_add_f32 v[44:45], v[78:79], v[68:69] neg_lo:[0,1] neg_hi:[0,1]
	v_pk_add_f32 v[48:49], v[66:67], v[42:43]
	v_xor_b32_e32 v42, 0x80000000, v29
	v_mov_b32_e32 v43, v28
	v_xor_b32_e32 v54, 0x80000000, v45
	v_mov_b32_e32 v55, v44
	v_pk_mul_f32 v[42:43], v[88:89], v[42:43] op_sel_hi:[0,1]
	v_pk_mul_f32 v[54:55], v[84:85], v[54:55] op_sel_hi:[0,1]
	v_pk_fma_f32 v[28:29], v[88:89], v[28:29], v[42:43] op_sel_hi:[0,1,1]
	v_pk_add_f32 v[42:43], v[78:79], v[68:69]
	v_pk_fma_f32 v[68:69], v[92:93], v[44:45], v[54:55] op_sel_hi:[0,1,1]
	v_pk_add_f32 v[54:55], v[74:75], v[36:37]
	v_pk_add_f32 v[36:37], v[74:75], v[36:37] neg_lo:[0,1] neg_hi:[0,1]
	v_pk_add_f32 v[58:59], v[56:57], v[32:33]
	v_xor_b32_e32 v44, 0x80000000, v37
	v_mov_b32_e32 v45, v36
	v_pk_mul_f32 v[44:45], v[84:85], v[44:45] op_sel_hi:[0,1]
	v_pk_add_f32 v[32:33], v[56:57], v[32:33] neg_lo:[0,1] neg_hi:[0,1]
	v_pk_fma_f32 v[74:75], v[92:93], v[36:37], v[44:45] op_sel_hi:[0,1,1] neg_lo:[1,0,0] neg_hi:[1,0,0]
	v_xor_b32_e32 v36, 0x80000000, v33
	v_mov_b32_e32 v37, v32
	v_pk_mul_f32 v[36:37], v[88:89], v[36:37] op_sel_hi:[0,1]
	v_pk_fma_f32 v[44:45], v[88:89], v[32:33], v[36:37] op_sel_hi:[0,1,1] neg_lo:[1,0,0] neg_hi:[1,0,0]
	v_pk_add_f32 v[36:37], v[70:71], v[50:51] neg_lo:[0,1] neg_hi:[0,1]
	v_pk_add_f32 v[32:33], v[70:71], v[50:51]
	v_xor_b32_e32 v50, 0x80000000, v37
	v_mov_b32_e32 v51, v36
	v_pk_mul_f32 v[50:51], v[92:93], v[50:51] op_sel_hi:[0,1]
	v_pk_add_f32 v[66:67], v[26:27], v[54:55]
	v_pk_add_f32 v[26:27], v[26:27], v[54:55] neg_lo:[0,1] neg_hi:[0,1]
	v_pk_fma_f32 v[50:51], v[84:85], v[36:37], v[50:51] op_sel_hi:[0,1,1] neg_lo:[1,0,0] neg_hi:[1,0,0]
	v_xor_b32_e32 v36, 0x80000000, v27
	v_mov_b32_e32 v37, v26
	v_pk_mul_f32 v[36:37], v[88:89], v[36:37] op_sel_hi:[0,1]
	v_pk_add_f32 v[70:71], v[42:43], v[32:33]
	v_pk_add_f32 v[32:33], v[42:43], v[32:33] neg_lo:[0,1] neg_hi:[0,1]
	v_pk_fma_f32 v[26:27], v[88:89], v[26:27], v[36:37] op_sel_hi:[0,1,1]
	v_xor_b32_e32 v36, 0x80000000, v33
	v_mov_b32_e32 v37, v32
	v_pk_mul_f32 v[36:37], v[88:89], v[36:37] op_sel_hi:[0,1]
	v_pk_fma_f32 v[36:37], v[88:89], v[32:33], v[36:37] op_sel_hi:[0,1,1] neg_lo:[1,0,0] neg_hi:[1,0,0]
	v_pk_add_f32 v[32:33], v[94:95], v[74:75] neg_lo:[0,1] neg_hi:[0,1]
	v_pk_add_f32 v[56:57], v[68:69], v[50:51]
	v_xor_b32_e32 v42, 0x80000000, v33
	v_mov_b32_e32 v43, v32
	v_pk_mul_f32 v[42:43], v[88:89], v[42:43] op_sel_hi:[0,1]
	v_pk_fma_f32 v[32:33], v[88:89], v[32:33], v[42:43] op_sel_hi:[0,1,1]
	v_pk_add_f32 v[42:43], v[68:69], v[50:51] neg_lo:[0,1] neg_hi:[0,1]
	v_pk_add_f32 v[54:55], v[94:95], v[74:75]
	v_xor_b32_e32 v50, 0x80000000, v43
	v_mov_b32_e32 v51, v42
	v_pk_mul_f32 v[50:51], v[88:89], v[50:51] op_sel_hi:[0,1]
	v_pk_fma_f32 v[42:43], v[88:89], v[42:43], v[50:51] op_sel_hi:[0,1,1] neg_lo:[1,0,0] neg_hi:[1,0,0]
	v_pk_add_f32 v[50:51], v[80:81], v[62:63] neg_lo:[0,1] neg_hi:[0,1]
	v_pk_add_f32 v[74:75], v[80:81], v[62:63]
	v_xor_b32_e32 v62, 0x80000000, v51
	v_mov_b32_e32 v63, v50
	v_pk_mul_f32 v[62:63], v[92:93], v[62:63] op_sel_hi:[0,1]
	v_pk_fma_f32 v[94:95], v[84:85], v[50:51], v[62:63] op_sel_hi:[0,1,1]
	v_pk_add_f32 v[50:51], v[64:65], v[60:61] neg_lo:[0,1] neg_hi:[0,1]
	v_pk_add_f32 v[68:69], v[64:65], v[60:61]
	v_xor_b32_e32 v60, 0x80000000, v51
	v_mov_b32_e32 v61, v50
	v_pk_mul_f32 v[60:61], v[88:89], v[60:61] op_sel_hi:[0,1]
	v_pk_fma_f32 v[50:51], v[88:89], v[50:51], v[60:61] op_sel_hi:[0,1,1]
	v_pk_add_f32 v[60:61], v[76:77], v[100:101] neg_lo:[0,1] neg_hi:[0,1]
	v_pk_add_f32 v[64:65], v[76:77], v[100:101]
	v_xor_b32_e32 v62, 0x80000000, v61
	v_mov_b32_e32 v63, v60
	v_pk_mul_f32 v[62:63], v[84:85], v[62:63] op_sel_hi:[0,1]
	v_pk_fma_f32 v[96:97], v[92:93], v[60:61], v[62:63] op_sel_hi:[0,1,1]
	v_pk_add_f32 v[60:61], v[72:73], v[86:87] neg_lo:[0,1] neg_hi:[0,1]
	v_pk_add_f32 v[76:77], v[52:53], v[46:47]
	v_pk_add_f32 v[46:47], v[52:53], v[46:47] neg_lo:[0,1] neg_hi:[0,1]
	v_pk_add_f32 v[62:63], v[72:73], v[86:87]
	v_xor_b32_e32 v72, 0x80000000, v61
	v_mov_b32_e32 v73, v60
	v_xor_b32_e32 v52, 0x80000000, v47
	v_mov_b32_e32 v53, v46
	v_pk_mul_f32 v[72:73], v[84:85], v[72:73] op_sel_hi:[0,1]
	v_pk_mul_f32 v[52:53], v[88:89], v[52:53] op_sel_hi:[0,1]
	v_pk_fma_f32 v[86:87], v[92:93], v[60:61], v[72:73] op_sel_hi:[0,1,1] neg_lo:[1,0,0] neg_hi:[1,0,0]
	v_pk_fma_f32 v[60:61], v[88:89], v[46:47], v[52:53] op_sel_hi:[0,1,1] neg_lo:[1,0,0] neg_hi:[1,0,0]
	v_pk_add_f32 v[46:47], v[98:99], v[90:91]
	v_pk_add_f32 v[52:53], v[98:99], v[90:91] neg_lo:[0,1] neg_hi:[0,1]
	v_pk_add_f32 v[80:81], v[64:65], v[46:47]
	v_pk_add_f32 v[46:47], v[64:65], v[46:47] neg_lo:[0,1] neg_hi:[0,1]
	v_xor_b32_e32 v72, 0x80000000, v53
	v_xor_b32_e32 v64, 0x80000000, v47
	v_mov_b32_e32 v65, v46
	v_pk_mul_f32 v[64:65], v[88:89], v[64:65] op_sel_hi:[0,1]
	v_mov_b32_e32 v73, v52
	v_pk_fma_f32 v[64:65], v[88:89], v[46:47], v[64:65] op_sel_hi:[0,1,1] neg_lo:[1,0,0] neg_hi:[1,0,0]
	v_pk_add_f32 v[46:47], v[94:95], v[86:87] neg_lo:[0,1] neg_hi:[0,1]
	v_pk_mul_f32 v[72:73], v[92:93], v[72:73] op_sel_hi:[0,1]
	v_pk_add_f32 v[78:79], v[74:75], v[62:63]
	v_pk_add_f32 v[62:63], v[74:75], v[62:63] neg_lo:[0,1] neg_hi:[0,1]
	v_xor_b32_e32 v74, 0x80000000, v47
	v_mov_b32_e32 v75, v46
	v_pk_fma_f32 v[52:53], v[84:85], v[52:53], v[72:73] op_sel_hi:[0,1,1] neg_lo:[1,0,0] neg_hi:[1,0,0]
	v_pk_mul_f32 v[74:75], v[88:89], v[74:75] op_sel_hi:[0,1]
	v_pk_fma_f32 v[46:47], v[88:89], v[46:47], v[74:75] op_sel_hi:[0,1,1]
	v_pk_add_f32 v[74:75], v[96:97], v[52:53]
	v_pk_add_f32 v[52:53], v[96:97], v[52:53] neg_lo:[0,1] neg_hi:[0,1]
	v_sub_f32_e32 v34, v16, v18
	v_xor_b32_e32 v84, 0x80000000, v53
	v_mov_b32_e32 v85, v52
	v_pk_mul_f32 v[84:85], v[88:89], v[84:85] op_sel_hi:[0,1]
	v_sub_f32_e32 v25, v33, v43
	v_sub_f32_e32 v43, v31, v35
	v_sub_f32_e32 v35, v51, v61
	v_pk_fma_f32 v[52:53], v[88:89], v[52:53], v[84:85] op_sel_hi:[0,1,1] neg_lo:[1,0,0] neg_hi:[1,0,0]
	v_sub_f32_e32 v51, v34, v82
	v_sub_f32_e32 v13, v49, v59
	v_sub_f32_e32 v10, v47, v53
	v_add_f32_e32 v49, v68, v76
	v_add_f32_e32 v53, v51, v30
	v_sub_f32_e32 v23, v27, v37
	v_sub_f32_e32 v27, v55, v57
	v_add_f32_e32 v40, v78, v80
	v_add_f32_e32 v55, v53, v49
	v_add_f32_e32 v16, v55, v40
	v_sub_f32_e32 v41, v39, v41
	v_add_f32_e32 v48, v48, v58
	v_add_f32_e32 v21, v20, v38
	global_store_dword v[14:15], v16, off offset:2048
	v_add_co_u32_e32 v16, vcc, s85, v14
	v_xor_b32_e32 v72, 0x80000000, v63
	v_mov_b32_e32 v73, v62
	v_add_f32_e32 v47, v66, v70
	v_add_f32_e32 v24, v21, v48
	v_add_f32_e32 v28, v28, v44
	v_sub_f32_e32 v44, v22, v41
	v_addc_co_u32_e32 v17, vcc, 0, v15, vcc
	v_pk_mul_f32 v[72:73], v[88:89], v[72:73] op_sel_hi:[0,1]
	v_add_f32_e32 v19, v24, v47
	v_add_f32_e32 v54, v54, v56
	v_add_f32_e32 v56, v44, v28
	v_add_co_u32_e32 v18, vcc, s84, v14
	v_add_f32_e32 v34, v34, v82
	v_pk_fma_f32 v[62:63], v[88:89], v[62:63], v[72:73] op_sel_hi:[0,1,1]
	v_pk_add_f32 v[72:73], v[94:95], v[86:87]
	global_store_dword v[14:15], v19, off
	v_add_f32_e32 v57, v56, v54
	v_addc_co_u32_e32 v19, vcc, 0, v15, vcc
	v_add_f32_e32 v50, v50, v60
	v_sub_f32_e32 v58, v34, v43
	global_store_dword v[18:19], v57, off offset:-4096
	v_add_f32_e32 v57, v72, v74
	v_add_f32_e32 v59, v58, v50
	v_sub_f32_e32 v20, v20, v38
	v_sub_f32_e32 v37, v29, v45
	v_sub_f32_e32 v45, v69, v77
	v_add_f32_e32 v60, v59, v57
	v_add_f32_e32 v26, v26, v36
	v_sub_f32_e32 v36, v20, v13
	v_sub_f32_e32 v30, v51, v30
	global_store_dword v[16:17], v60, off offset:2048
	v_add_f32_e32 v16, v36, v26
	v_add_f32_e32 v38, v62, v64
	v_sub_f32_e32 v51, v30, v45
	global_store_dword v[18:19], v16, off
	v_add_f32_e32 v16, v51, v38
	global_store_dword v[18:19], v16, off offset:2048
	v_add_co_u32_e32 v16, vcc, s61, v14
	v_add_f32_e32 v22, v22, v41
	s_nop 0
	v_addc_co_u32_e32 v17, vcc, 0, v15, vcc
	v_add_f32_e32 v32, v32, v42
	v_sub_f32_e32 v41, v22, v37
	v_add_co_u32_e32 v18, vcc, s45, v14
	v_add_f32_e32 v42, v41, v32
	s_nop 0
	v_addc_co_u32_e32 v19, vcc, 0, v15, vcc
	v_add_f32_e32 v34, v34, v43
	global_store_dword v[18:19], v42, off offset:-4096
	v_add_f32_e32 v42, v46, v52
	v_sub_f32_e32 v43, v34, v35
	v_sub_f32_e32 v39, v67, v71
	v_add_f32_e32 v46, v43, v42
	v_sub_f32_e32 v21, v21, v48
	v_sub_f32_e32 v33, v79, v81
	global_store_dword v[16:17], v46, off offset:2048
	v_sub_f32_e32 v16, v21, v39
	v_sub_f32_e32 v46, v53, v49
	global_store_dword v[18:19], v16, off
	v_sub_f32_e32 v16, v46, v33
	global_store_dword v[18:19], v16, off offset:2048
	v_add_co_u32_e32 v16, vcc, s86, v14
	v_sub_f32_e32 v28, v44, v28
	s_nop 0
	v_addc_co_u32_e32 v17, vcc, 0, v15, vcc
	v_add_co_u32_e32 v18, vcc, s88, v14
	v_sub_f32_e32 v44, v28, v27
	s_nop 0
	v_addc_co_u32_e32 v19, vcc, 0, v15, vcc
	v_sub_f32_e32 v31, v73, v75
	global_store_dword v[18:19], v44, off offset:-4096
	v_sub_f32_e32 v44, v58, v50
	v_sub_f32_e32 v48, v44, v31
	v_add_f32_e32 v20, v20, v13
	v_sub_f32_e32 v29, v63, v65
	global_store_dword v[16:17], v48, off offset:2048
	v_sub_f32_e32 v13, v20, v23
	v_add_f32_e32 v30, v30, v45
	v_add_co_u32_e32 v16, vcc, s90, v14
	global_store_dword v[18:19], v13, off
	v_sub_f32_e32 v13, v30, v29
	v_addc_co_u32_e32 v17, vcc, 0, v15, vcc
	global_store_dword v[18:19], v13, off offset:2048
	v_add_f32_e32 v22, v22, v37
	v_add_co_u32_e32 v18, vcc, s8, v14
	v_sub_f32_e32 v13, v22, v25
	s_nop 0
	v_addc_co_u32_e32 v19, vcc, 0, v15, vcc
	global_store_dword v[18:19], v13, off offset:-4096
	v_add_f32_e32 v13, v34, v35
	v_sub_f32_e32 v34, v13, v10
	global_store_dword v[16:17], v34, off offset:2048
	v_sub_f32_e32 v16, v24, v47
	global_store_dword v[18:19], v16, off
	v_sub_f32_e32 v16, v55, v40
	global_store_dword v[18:19], v16, off offset:2048
	v_add_co_u32_e32 v16, vcc, s9, v14
	v_sub_f32_e32 v24, v56, v54
	s_nop 0
	v_addc_co_u32_e32 v17, vcc, 0, v15, vcc
	v_add_co_u32_e32 v18, vcc, s7, v14
	v_add_f32_e32 v10, v13, v10
	s_nop 0
	v_addc_co_u32_e32 v19, vcc, 0, v15, vcc
	global_store_dword v[18:19], v24, off offset:-4096
	v_sub_f32_e32 v24, v59, v57
	global_store_dword v[16:17], v24, off offset:2048
	v_sub_f32_e32 v16, v36, v26
	global_store_dword v[18:19], v16, off
	v_sub_f32_e32 v16, v51, v38
	global_store_dword v[18:19], v16, off offset:2048
	v_add_co_u32_e32 v16, vcc, s5, v14
	v_sub_f32_e32 v24, v41, v32
	s_nop 0
	v_addc_co_u32_e32 v17, vcc, 0, v15, vcc
	v_add_co_u32_e32 v18, vcc, s6, v14
	s_nop 1
	v_addc_co_u32_e32 v19, vcc, 0, v15, vcc
	global_store_dword v[18:19], v24, off offset:-4096
	v_sub_f32_e32 v24, v43, v42
	global_store_dword v[16:17], v24, off offset:2048
	v_add_f32_e32 v16, v21, v39
	global_store_dword v[18:19], v16, off
	v_add_f32_e32 v16, v46, v33
	global_store_dword v[18:19], v16, off offset:2048
	v_add_co_u32_e32 v16, vcc, s4, v14
	v_add_f32_e32 v21, v28, v27
	s_nop 0
	v_addc_co_u32_e32 v17, vcc, 0, v15, vcc
	v_add_co_u32_e32 v18, vcc, s1, v14
	s_nop 1
	v_addc_co_u32_e32 v19, vcc, 0, v15, vcc
	global_store_dword v[18:19], v21, off offset:-4096
	v_add_f32_e32 v21, v44, v31
	global_store_dword v[16:17], v21, off offset:2048
	v_add_f32_e32 v16, v20, v23
	global_store_dword v[18:19], v16, off
	v_add_f32_e32 v16, v30, v29
	v_add_co_u32_e32 v14, vcc, s0, v14
	global_store_dword v[18:19], v16, off offset:2048
	v_add_f32_e32 v16, v22, v25
	v_addc_co_u32_e32 v15, vcc, 0, v15, vcc
	global_store_dword v[14:15], v16, off
	global_store_dword v[14:15], v10, off offset:2048
	v_mov_b32_e32 v10, v184
	v_mov_b32_e32 v14, v185
	v_mov_b32_e32 v18, v1
	s_movk_i32 s0, 0xfe00
	v_sub_u32_e32 v13, 0x4000, v18
	v_cmp_eq_u32_e32 vcc, 0, v18
	v_cmp_eq_u32_e64 s[0:1], s0, v18
	v_cmp_eq_u32_e64 s[4:5], s50, v18
	v_cndmask_b32_e64 v20, v13, 0, vcc
	v_sub_u32_e32 v13, 0x3e00, v18
	v_cndmask_b32_e64 v22, v13, 0, s[0:1]
	v_sub_u32_e32 v13, 0x3c00, v18
	v_ashrrev_i32_e32 v21, 31, v20
	v_ashrrev_i32_e32 v23, 31, v22
	v_cndmask_b32_e64 v24, v13, 0, s[4:5]
	v_lshl_add_u64 v[20:21], v[20:21], 1, s[2:3]
	v_lshl_add_u64 v[22:23], v[22:23], 1, s[2:3]
	v_ashrrev_i32_e32 v25, 31, v24
	v_sub_u32_e32 v13, 0x3a00, v18
	v_cmp_eq_u32_e64 s[6:7], s51, v18
	v_lshl_add_u64 v[24:25], v[24:25], 1, s[2:3]
	global_load_ushort v15, v[20:21], off
	s_nop 0
	global_load_ushort v22, v[22:23], off
	s_nop 0
	global_load_ushort v23, v[24:25], off
	v_cndmask_b32_e64 v20, v13, 0, s[6:7]
	v_ashrrev_i32_e32 v21, 31, v20
	v_ashrrev_i32_e32 v19, 31, v18
	v_lshl_add_u64 v[20:21], v[20:21], 1, s[2:3]
	v_lshl_add_u64 v[16:17], v[18:19], 1, s[78:79]
	global_load_ushort v20, v[20:21], off
	s_nop 0
	global_load_ushort v13, v[16:17], off offset:3072
	v_sub_u32_e32 v24, 0x3800, v18
	v_sub_u32_e32 v26, 0x3600, v18
	v_sub_u32_e32 v28, 0x3400, v18
	v_sub_u32_e32 v32, 0x3200, v18
	v_cmp_eq_u32_e64 s[8:9], s60, v18
	v_cmp_eq_u32_e64 s[10:11], s10, v18
	s_mov_b32 s78, s69
	s_mov_b32 s79, s68
	s_mov_b32 s50, s21
	s_mov_b32 s51, s20
	s_mov_b32 s60, s25
	s_waitcnt vmcnt(4)
	v_lshlrev_b32_e32 v15, 16, v15
	v_cndmask_b32_e64 v19, -v15, v15, vcc
	s_waitcnt vmcnt(3)
	v_lshlrev_b32_e32 v15, 16, v22
	v_add_co_u32_e32 v22, vcc, s85, v16
	v_cndmask_b32_e64 v31, -v15, v15, s[0:1]
	s_waitcnt vmcnt(2)
	v_lshlrev_b32_e32 v15, 16, v23
	v_addc_co_u32_e32 v23, vcc, 0, v17, vcc
	v_cndmask_b32_e64 v30, -v15, v15, s[4:5]
	s_waitcnt vmcnt(1)
	v_lshlrev_b32_e32 v15, 16, v20
	v_add_co_u32_e32 v20, vcc, s84, v16
	v_cndmask_b32_e64 v15, -v15, v15, s[6:7]
	s_nop 0
	v_addc_co_u32_e32 v21, vcc, 0, v17, vcc
	v_cmp_eq_u32_e64 s[6:7], s56, v18
	v_cmp_eq_u32_e64 s[4:5], s57, v18
	v_cmp_eq_u32_e64 s[0:1], s58, v18
	v_cndmask_b32_e64 v24, v24, 0, s[6:7]
	v_cndmask_b32_e64 v26, v26, 0, s[4:5]
	v_cndmask_b32_e64 v28, v28, 0, s[0:1]
	v_cmp_eq_u32_e32 vcc, s59, v18
	v_ashrrev_i32_e32 v25, 31, v24
	v_ashrrev_i32_e32 v27, 31, v26
	v_ashrrev_i32_e32 v29, 31, v28
	v_cndmask_b32_e64 v32, v32, 0, vcc
	v_lshl_add_u64 v[24:25], v[24:25], 1, s[2:3]
	v_lshl_add_u64 v[26:27], v[26:27], 1, s[2:3]
	v_lshl_add_u64 v[28:29], v[28:29], 1, s[2:3]
	v_ashrrev_i32_e32 v33, 31, v32
	v_lshl_add_u64 v[32:33], v[32:33], 1, s[2:3]
	global_load_ushort v34, v[24:25], off
	s_nop 0
	global_load_ushort v26, v[26:27], off
	s_nop 0
	global_load_ushort v27, v[28:29], off
	s_nop 0
	global_load_ushort v28, v[32:33], off
	v_sub_u32_e32 v24, 0x3000, v18
	v_cndmask_b32_e64 v24, v24, 0, s[8:9]
	v_ashrrev_i32_e32 v25, 31, v24
	v_lshl_add_u64 v[24:25], v[24:25], 1, s[2:3]
	global_load_ushort v24, v[24:25], off
	s_nop 0
	global_load_ushort v33, v[22:23], off offset:3072
	s_waitcnt vmcnt(6)
	v_lshlrev_b32_e32 v13, 16, v13
	s_mov_b32 s56, s39
	s_mov_b32 s57, s38
	s_mov_b32 s58, s19
	s_mov_b32 s59, s18
	s_waitcnt vmcnt(5)
	v_lshlrev_b32_e32 v25, 16, v34
	v_cndmask_b32_e64 v32, -v25, v25, s[6:7]
	s_waitcnt vmcnt(4)
	v_lshlrev_b32_e32 v25, 16, v26
	v_cndmask_b32_e64 v36, -v25, v25, s[4:5]
	s_waitcnt vmcnt(3)
	v_lshlrev_b32_e32 v25, 16, v27
	v_cndmask_b32_e64 v37, -v25, v25, s[0:1]
	v_add_co_u32_e64 v26, s[0:1], s61, v16
	s_waitcnt vmcnt(2)
	v_lshlrev_b32_e32 v25, 16, v28
	s_waitcnt vmcnt(1)
	v_lshlrev_b32_e32 v24, 16, v24
	v_addc_co_u32_e64 v27, s[0:1], 0, v17, s[0:1]
	v_cndmask_b32_e64 v35, -v25, v25, vcc
	v_cndmask_b32_e64 v34, -v24, v24, s[8:9]
	v_sub_u32_e32 v24, 0x2e00, v18
	v_cmp_eq_u32_e32 vcc, s62, v18
	v_sub_u32_e32 v28, 0x2c00, v18
	v_cmp_eq_u32_e64 s[0:1], s63, v18
	v_cndmask_b32_e64 v24, v24, 0, vcc
	v_ashrrev_i32_e32 v25, 31, v24
	v_cndmask_b32_e64 v28, v28, 0, s[0:1]
	v_ashrrev_i32_e32 v29, 31, v28
	v_lshl_add_u64 v[24:25], v[24:25], 1, s[2:3]
	v_lshl_add_u64 v[28:29], v[28:29], 1, s[2:3]
	global_load_ushort v38, v[24:25], off
	s_nop 0
	global_load_ushort v28, v[28:29], off
	v_sub_u32_e32 v24, 0x2a00, v18
	v_cmp_eq_u32_e64 s[4:5], s64, v18
	v_cmp_eq_u32_e64 s[6:7], s65, v18
	s_mov_b32 s62, s29
	v_cndmask_b32_e64 v24, v24, 0, s[4:5]
	v_ashrrev_i32_e32 v25, 31, v24
	v_lshl_add_u64 v[24:25], v[24:25], 1, s[2:3]
	global_load_ushort v29, v[24:25], off
	v_sub_u32_e32 v24, 0x2800, v18
	v_cndmask_b32_e64 v24, v24, 0, s[6:7]
	v_ashrrev_i32_e32 v25, 31, v24
	v_lshl_add_u64 v[24:25], v[24:25], 1, s[2:3]
	global_load_ushort v41, v[26:27], off offset:1024
	global_load_ushort v40, v[26:27], off offset:2048
	global_load_ushort v39, v[26:27], off offset:3072
	global_load_ushort v42, v[24:25], off
	v_sub_u32_e32 v26, 0x2600, v18
	s_mov_b32 s63, s28
	s_mov_b32 s61, s24
	s_waitcnt vmcnt(6)
	v_lshlrev_b32_e32 v24, 16, v38
	v_cndmask_b32_e64 v45, -v24, v24, vcc
	s_waitcnt vmcnt(5)
	v_lshlrev_b32_e32 v24, 16, v28
	v_cndmask_b32_e64 v44, -v24, v24, s[0:1]
	s_movk_i32 s0, 0xe600
	v_sub_u32_e32 v38, 0x2200, v18
	s_waitcnt vmcnt(4)
	v_lshlrev_b32_e32 v24, 16, v29
	v_cndmask_b32_e64 v43, -v24, v24, s[4:5]
	v_add_co_u32_e32 v24, vcc, s45, v16
	s_nop 1
	v_addc_co_u32_e32 v25, vcc, 0, v17, vcc
	v_cmp_eq_u32_e32 vcc, s0, v18
	s_movk_i32 s0, 0xe400
	s_nop 0
	v_cndmask_b32_e64 v26, v26, 0, vcc
	v_ashrrev_i32_e32 v27, 31, v26
	v_lshl_add_u64 v[26:27], v[26:27], 1, s[2:3]
	global_load_ushort v26, v[26:27], off
	s_waitcnt vmcnt(1)
	v_lshlrev_b32_e32 v27, 16, v42
	v_cndmask_b32_e64 v49, -v27, v27, s[6:7]
	s_waitcnt vmcnt(0)
	v_lshlrev_b32_e32 v26, 16, v26
	v_cndmask_b32_e64 v50, -v26, v26, vcc
	v_cmp_eq_u32_e32 vcc, s0, v18
	v_add_co_u32_e64 v28, s[0:1], s86, v16
	v_sub_u32_e32 v26, 0x2400, v18
	s_nop 0
	v_addc_co_u32_e64 v29, s[0:1], 0, v17, s[0:1]
	s_movk_i32 s0, 0xe200
	s_nop 0
	v_cmp_eq_u32_e64 s[8:9], s0, v18
	s_movk_i32 s0, 0xe000
	v_cmp_eq_u32_e64 s[6:7], s0, v18
	v_cndmask_b32_e64 v46, v38, 0, s[8:9]
	v_sub_u32_e32 v38, 0x2000, v18
	s_movk_i32 s0, 0xde00
	v_cndmask_b32_e64 v52, v38, 0, s[6:7]
	v_sub_u32_e32 v38, 0x1e00, v18
	v_cmp_eq_u32_e64 s[4:5], s0, v18
	s_movk_i32 s0, 0xdc00
	v_cndmask_b32_e64 v26, v26, 0, vcc
	v_cndmask_b32_e64 v54, v38, 0, s[4:5]
	v_sub_u32_e32 v38, 0x1c00, v18
	v_cmp_eq_u32_e64 s[0:1], s0, v18
	v_ashrrev_i32_e32 v27, 31, v26
	v_ashrrev_i32_e32 v47, 31, v46
	v_cndmask_b32_e64 v56, v38, 0, s[0:1]
	v_lshl_add_u64 v[26:27], v[26:27], 1, s[2:3]
	v_lshl_add_u64 v[46:47], v[46:47], 1, s[2:3]
	v_ashrrev_i32_e32 v53, 31, v52
	v_ashrrev_i32_e32 v55, 31, v54
	v_ashrrev_i32_e32 v57, 31, v56
	v_lshl_add_u64 v[52:53], v[52:53], 1, s[2:3]
	v_lshl_add_u64 v[54:55], v[54:55], 1, s[2:3]
	v_lshl_add_u64 v[56:57], v[56:57], 1, s[2:3]
	global_load_ushort v38, v[26:27], off
	global_load_ushort v42, v[46:47], off
	s_nop 0
	global_load_ushort v46, v[52:53], off
	global_load_ushort v47, v[54:55], off
	global_load_ushort v48, v[56:57], off
	v_sub_u32_e32 v26, 0x1a00, v18
	v_cndmask_b32_e64 v26, v26, 0, s[10:11]
	v_ashrrev_i32_e32 v27, 31, v26
	v_lshl_add_u64 v[26:27], v[26:27], 1, s[2:3]
	global_load_ushort v26, v[26:27], off
	s_nop 0
	global_load_ushort v53, v[28:29], off offset:1024
	global_load_ushort v51, v[28:29], off offset:2048
	s_waitcnt vmcnt(7)
	v_lshlrev_b32_e32 v27, 16, v38
	v_cndmask_b32_e64 v61, -v27, v27, vcc
	s_waitcnt vmcnt(6)
	v_lshlrev_b32_e32 v27, 16, v42
	v_cndmask_b32_e64 v63, -v27, v27, s[8:9]
	s_waitcnt vmcnt(5)
	v_lshlrev_b32_e32 v27, 16, v46
	v_cndmask_b32_e64 v90, -v27, v27, s[6:7]
	s_waitcnt vmcnt(4)
	v_lshlrev_b32_e32 v27, 16, v47
	v_cndmask_b32_e64 v59, -v27, v27, s[4:5]
	s_waitcnt vmcnt(3)
	v_lshlrev_b32_e32 v27, 16, v48
	v_cndmask_b32_e64 v57, -v27, v27, s[0:1]
	s_movk_i32 s0, 0xd800
	v_sub_u32_e32 v38, 0x1800, v18
	v_cmp_eq_u32_e64 s[8:9], s0, v18
	s_movk_i32 s0, 0xd600
	s_waitcnt vmcnt(2)
	v_lshlrev_b32_e32 v26, 16, v26
	v_cndmask_b32_e64 v46, v38, 0, s[8:9]
	v_sub_u32_e32 v38, 0x1600, v18
	v_cmp_eq_u32_e64 s[6:7], s0, v18
	s_movk_i32 s0, 0xd400
	v_cndmask_b32_e64 v55, -v26, v26, s[10:11]
	v_add_co_u32_e32 v26, vcc, s88, v16
	v_cndmask_b32_e64 v64, v38, 0, s[6:7]
	v_sub_u32_e32 v38, 0x1400, v18
	v_cmp_eq_u32_e64 s[4:5], s0, v18
	s_movk_i32 s0, 0xd200
	v_addc_co_u32_e32 v27, vcc, 0, v17, vcc
	v_cndmask_b32_e64 v66, v38, 0, s[4:5]
	v_sub_u32_e32 v38, 0x1200, v18
	v_cmp_eq_u32_e64 s[0:1], s0, v18
	s_movk_i32 s10, 0xd000
	v_cmp_eq_u32_e32 vcc, s10, v18
	v_cndmask_b32_e64 v68, v38, 0, s[0:1]
	v_sub_u32_e32 v38, 0x1000, v18
	v_ashrrev_i32_e32 v47, 31, v46
	v_cndmask_b32_e64 v70, v38, 0, vcc
	v_lshl_add_u64 v[46:47], v[46:47], 1, s[2:3]
	v_ashrrev_i32_e32 v65, 31, v64
	v_ashrrev_i32_e32 v67, 31, v66
	v_ashrrev_i32_e32 v69, 31, v68
	v_ashrrev_i32_e32 v71, 31, v70
	s_movk_i32 s10, 0xce00
	v_lshl_add_u64 v[64:65], v[64:65], 1, s[2:3]
	v_lshl_add_u64 v[66:67], v[66:67], 1, s[2:3]
	v_lshl_add_u64 v[68:69], v[68:69], 1, s[2:3]
	v_lshl_add_u64 v[70:71], v[70:71], 1, s[2:3]
	global_load_ushort v38, v[46:47], off
	global_load_ushort v42, v[64:65], off
	global_load_ushort v48, v[66:67], off
	global_load_ushort v52, v[68:69], off
	global_load_ushort v54, v[70:71], off
	v_sub_u32_e32 v46, 0xe00, v18
	v_cmp_eq_u32_e64 s[12:13], s10, v18
	s_movk_i32 s10, 0xcc00
	v_cmp_eq_u32_e64 s[10:11], s10, v18
	v_cndmask_b32_e64 v46, v46, 0, s[12:13]
	v_ashrrev_i32_e32 v47, 31, v46
	v_lshl_add_u64 v[46:47], v[46:47], 1, s[2:3]
	global_load_ushort v56, v[46:47], off
	v_sub_u32_e32 v46, 0xc00, v18
	v_cndmask_b32_e64 v46, v46, 0, s[10:11]
	v_ashrrev_i32_e32 v47, 31, v46
	v_lshl_add_u64 v[46:47], v[46:47], 1, s[2:3]
	global_load_ushort v46, v[46:47], off
	s_nop 0
	global_load_ushort v91, v[28:29], off offset:3072
	s_waitcnt vmcnt(7)
	v_lshlrev_b32_e32 v28, 16, v38
	v_cndmask_b32_e64 v97, -v28, v28, s[8:9]
	s_waitcnt vmcnt(6)
	v_lshlrev_b32_e32 v28, 16, v42
	v_cndmask_b32_e64 v96, -v28, v28, s[6:7]
	s_waitcnt vmcnt(5)
	v_lshlrev_b32_e32 v28, 16, v48
	v_cndmask_b32_e64 v94, -v28, v28, s[4:5]
	s_waitcnt vmcnt(4)
	v_lshlrev_b32_e32 v28, 16, v52
	v_cndmask_b32_e64 v93, -v28, v28, s[0:1]
	s_waitcnt vmcnt(3)
	v_lshlrev_b32_e32 v28, 16, v54
	v_cndmask_b32_e64 v92, -v28, v28, vcc
	s_movk_i32 s0, 0xca00
	v_cmp_eq_u32_e64 s[0:1], s0, v18
	s_waitcnt vmcnt(2)
	v_lshlrev_b32_e32 v28, 16, v56
	v_cndmask_b32_e64 v95, -v28, v28, s[12:13]
	v_sub_u32_e32 v28, 0xa00, v18
	v_cndmask_b32_e64 v28, v28, 0, s[0:1]
	v_ashrrev_i32_e32 v29, 31, v28
	v_lshl_add_u64 v[28:29], v[28:29], 1, s[2:3]
	global_load_ushort v38, v[28:29], off
	s_waitcnt vmcnt(2)
	v_lshlrev_b32_e32 v28, 16, v46
	v_cndmask_b32_e64 v106, -v28, v28, s[10:11]
	v_add_co_u32_e32 v28, vcc, s90, v16
	s_movk_i32 s4, 0xc400
	s_nop 0
	v_addc_co_u32_e32 v29, vcc, 0, v17, vcc
	v_sub_u32_e32 v42, 0x400, v18
	v_cmp_eq_u32_e32 vcc, s4, v18
	s_movk_i32 s4, 0xc800
	v_cmp_eq_u32_e64 s[4:5], s4, v18
	v_cndmask_b32_e64 v46, v42, 0, vcc
	v_sub_u32_e32 v42, 0x800, v18
	v_ashrrev_i32_e32 v47, 31, v46
	v_cndmask_b32_e64 v64, v42, 0, s[4:5]
	v_lshl_add_u64 v[46:47], v[46:47], 1, s[2:3]
	v_ashrrev_i32_e32 v65, 31, v64
	v_lshl_add_u64 v[64:65], v[64:65], 1, s[2:3]
	global_load_ushort v42, v[46:47], off
	s_nop 0
	global_load_ushort v46, v[64:65], off
	global_load_ushort v110, v[28:29], off
	global_load_ushort v112, v[28:29], off offset:1024
	global_load_ushort v114, v[28:29], off offset:2048
	global_load_ushort v116, v[28:29], off offset:3072
	s_mov_b32 s10, 0x3f74fa0b
	s_mov_b32 s11, 0xbe94a031
	s_mov_b32 s80, s11
	s_mov_b32 s81, s10
	v_add_f32_e32 v52, v15, v13
	s_mov_b32 s12, 0x3e94a031
	s_mov_b32 s13, 0xbf74fa0b
	s_mov_b32 s64, s13
	s_mov_b32 s65, s12
	s_mov_b32 s8, 0x3e47c5c2
	s_mov_b32 s9, 0xbf7b14be
	s_mov_b32 s30, s9
	s_mov_b32 s31, s8
	s_mov_b32 s6, 0x3f7b14be
	s_mov_b32 s7, 0xbe47c5c2
	s_mov_b32 s6, s9
	s_waitcnt vmcnt(6)
	v_lshlrev_b32_e32 v28, 16, v38
	v_cndmask_b32_e64 v108, -v28, v28, s[0:1]
	s_movk_i32 s0, 0xc600
	v_sub_u32_e32 v28, 0x600, v18
	v_sub_u32_e32 v38, 0x200, v18
	s_waitcnt vmcnt(4)
	v_lshlrev_b32_e32 v29, 16, v46
	v_cndmask_b32_e64 v111, -v29, v29, s[4:5]
	v_cmp_eq_u32_e64 s[4:5], s0, v18
	s_movk_i32 s0, 0xc200
	v_cmp_eq_u32_e64 s[0:1], s0, v18
	v_cndmask_b32_e64 v28, v28, 0, s[4:5]
	v_ashrrev_i32_e32 v29, 31, v28
	v_cndmask_b32_e64 v46, v38, 0, s[0:1]
	v_lshl_add_u64 v[28:29], v[28:29], 1, s[2:3]
	v_ashrrev_i32_e32 v47, 31, v46
	v_lshl_add_u64 v[46:47], v[46:47], 1, s[2:3]
	global_load_ushort v18, v[16:17], off
	s_nop 0
	global_load_ushort v28, v[28:29], off
	s_nop 0
	global_load_ushort v29, v[16:17], off offset:1024
	s_nop 0
	global_load_ushort v17, v[16:17], off offset:2048
	s_nop 0
	global_load_ushort v38, v[46:47], off
	global_load_ushort v56, v[20:21], off offset:1024
	global_load_ushort v58, v[20:21], off offset:2048
	global_load_ushort v60, v[20:21], off offset:3072
	global_load_ushort v62, v[24:25], off offset:-4096
	global_load_ushort v98, v[24:25], off
	global_load_ushort v48, v[20:21], off offset:-4096
	global_load_ushort v64, v[22:23], off offset:1024
	global_load_ushort v68, v[22:23], off offset:2048
	s_nop 0
	global_load_ushort v21, v[20:21], off
	v_lshlrev_b32_e32 v22, 16, v42
	v_cndmask_b32_e64 v115, -v22, v22, vcc
	v_pk_mul_f32 v[22:23], v[14:15], s[78:79] op_sel_hi:[0,1] neg_lo:[1,0]
	s_mov_b64 vcc, s[66:67]
	s_mov_b32 s66, s71
	s_mov_b32 s67, s70
	s_mov_b32 s2, 0x3f7ec46d
	s_mov_b32 s3, 0xbdc8bd36
	s_waitcnt vmcnt(13)
	v_lshlrev_b32_e32 v16, 16, v18
	s_waitcnt vmcnt(12)
	v_lshlrev_b32_e32 v18, 16, v28
	s_waitcnt vmcnt(11)
	v_lshlrev_b32_e32 v20, 16, v29
	s_waitcnt vmcnt(10)
	v_lshlrev_b32_e32 v17, 16, v17
	v_add_f32_e32 v20, v31, v20
	v_pk_fma_f32 v[28:29], v[10:11], s[68:69], v[22:23] op_sel_hi:[0,1,1]
	v_add_f32_e32 v22, v30, v17
	v_pk_mul_f32 v[30:31], v[14:15], s[66:67] op_sel_hi:[0,1] neg_lo:[1,0]
	v_pk_fma_f32 v[46:47], v[10:11], s[70:71], v[30:31] op_sel_hi:[0,1,1]
	v_pk_mul_f32 v[30:31], v[14:15], s[80:81] op_sel_hi:[0,1] neg_lo:[1,0]
	v_pk_fma_f32 v[88:89], v[10:11], s[10:11], v[30:31] op_sel_hi:[0,1,1]
	s_waitcnt vmcnt(3)
	v_lshlrev_b32_e32 v13, 16, v48
	v_pk_mul_f32 v[30:31], v[14:15], s[52:53] op_sel_hi:[0,1] neg_lo:[1,0]
	v_add_f32_e32 v16, v19, v16
	v_cndmask_b32_e64 v113, -v18, v18, s[4:5]
	v_pk_mul_f32 v[18:19], v[14:15], s[40:41] op_sel_hi:[0,1] neg_lo:[1,0]
	v_add_f32_e32 v54, v32, v13
	v_pk_fma_f32 v[66:67], v[10:11], s[94:95], v[30:31] op_sel_hi:[0,1,1]
	s_waitcnt vmcnt(2)
	v_lshlrev_b32_e32 v13, 16, v64
	v_pk_mul_f32 v[30:31], v[14:15], s[50:51] op_sel_hi:[0,1] neg_lo:[1,0]
	s_waitcnt vmcnt(1)
	v_lshlrev_b32_e32 v15, 16, v68
	v_lshlrev_b32_e32 v17, 16, v38
	v_add_f32_e32 v32, v36, v13
	global_load_ushort v13, v[24:25], off offset:1024
	v_add_f32_e32 v38, v37, v15
	global_load_ushort v15, v[24:25], off offset:2048
	v_lshlrev_b32_e32 v23, 16, v33
	s_waitcnt vmcnt(2)
	v_lshlrev_b32_e32 v21, 16, v21
	v_add_f32_e32 v42, v35, v23
	global_load_ushort v23, v[24:25], off offset:3072
	global_load_ushort v33, v[26:27], off
	v_add_f32_e32 v48, v34, v21
	v_lshlrev_b32_e32 v21, 16, v56
	v_add_f32_e32 v56, v45, v21
	global_load_ushort v21, v[26:27], off offset:-4096
	s_mov_b32 s68, s83
	s_mov_b32 s69, s82
	s_mov_b32 s70, s23
	s_mov_b32 s71, s22
	v_pk_fma_f32 v[64:65], v[10:11], s[20:21], v[30:31] op_sel_hi:[0,1,1]
	s_mov_b32 s94, s75
	s_mov_b32 s95, s74
	s_mov_b32 s4, 0x3dc8bd36
	s_mov_b32 s5, 0xbf7ec46d
	s_mov_b32 s34, s5
	s_mov_b32 s35, s4
	s_mov_b32 s2, s5
	v_cndmask_b32_e64 v17, -v17, v17, s[0:1]
	s_mov_b32 s0, s3
	s_mov_b32 s1, s5
	s_mov_b32 s10, s13
	s_mov_b32 s20, s23
	v_pk_fma_f32 v[18:19], v[10:11], s[46:47], v[18:19] op_sel_hi:[0,1,1]
	s_waitcnt vmcnt(4)
	v_lshlrev_b32_e32 v13, 16, v13
	s_waitcnt vmcnt(3)
	v_pk_mul_f32 v[24:25], v[14:15], s[56:57] op_sel_hi:[0,1] neg_lo:[1,0]
	v_pk_fma_f32 v[76:77], v[10:11], s[38:39], v[24:25] op_sel_hi:[0,1,1]
	v_pk_mul_f32 v[24:25], v[14:15], s[62:63] op_sel_hi:[0,1] neg_lo:[1,0]
	v_pk_fma_f32 v[82:83], v[10:11], s[28:29], v[24:25] op_sel_hi:[0,1,1]
	v_lshlrev_b32_e32 v24, 16, v58
	v_add_f32_e32 v58, v44, v24
	v_pk_mul_f32 v[24:25], v[14:15], s[68:69] op_sel_hi:[0,1] neg_lo:[1,0]
	v_pk_fma_f32 v[84:85], v[10:11], s[82:83], v[24:25] op_sel_hi:[0,1,1]
	v_lshlrev_b32_e32 v24, 16, v60
	v_add_f32_e32 v60, v43, v24
	v_pk_mul_f32 v[24:25], v[14:15], s[70:71] op_sel_hi:[0,1] neg_lo:[1,0]
	v_pk_fma_f32 v[86:87], v[10:11], s[22:23], v[24:25] op_sel_hi:[0,1,1]
	v_lshlrev_b32_e32 v24, 16, v62
	v_add_f32_e32 v62, v49, v24
	v_pk_mul_f32 v[24:25], v[14:15], s[58:59] op_sel_hi:[0,1] neg_lo:[1,0]
	v_pk_fma_f32 v[80:81], v[10:11], s[18:19], v[24:25] op_sel_hi:[0,1,1]
	v_lshlrev_b32_e32 v24, 16, v41
	v_add_f32_e32 v50, v50, v24
	v_pk_mul_f32 v[24:25], v[14:15], s[64:65] op_sel_hi:[0,1] neg_lo:[1,0]
	v_pk_fma_f32 v[78:79], v[10:11], s[12:13], v[24:25] op_sel_hi:[0,1,1]
	v_lshlrev_b32_e32 v25, 16, v39
	v_add_f32_e32 v44, v63, v25
	global_load_ushort v25, v[26:27], off offset:1024
	global_load_ushort v39, v[26:27], off offset:2048
	v_lshlrev_b32_e32 v24, 16, v40
	global_load_ushort v40, v[26:27], off offset:3072
	v_pk_mul_f32 v[30:31], v[14:15], s[60:61] op_sel_hi:[0,1] neg_lo:[1,0]
	v_pk_fma_f32 v[68:69], v[10:11], s[24:25], v[30:31] op_sel_hi:[0,1,1]
	v_pk_mul_f32 v[30:31], v[14:15], s[94:95] op_sel_hi:[0,1] neg_lo:[1,0]
	v_pk_fma_f32 v[74:75], v[10:11], s[74:75], v[30:31] op_sel_hi:[0,1,1]
	v_pk_mul_f32 v[30:31], v[14:15], s[30:31] op_sel_hi:[0,1] neg_lo:[1,0]
	v_pk_fma_f32 v[70:71], v[10:11], s[8:9], v[30:31] op_sel_hi:[0,1,1]
	v_pk_mul_f32 v[30:31], v[14:15], s[34:35] op_sel_hi:[0,1] neg_lo:[1,0]
	v_pk_fma_f32 v[72:73], v[10:11], s[4:5], v[30:31] op_sel_hi:[0,1,1]
	v_lshlrev_b32_e32 v30, 16, v98
	v_pk_mul_f32 v[34:35], v[14:15], s[36:37] op_sel_hi:[0,1] neg_lo:[1,0]
	v_add_f32_e32 v30, v90, v30
	v_pk_fma_f32 v[34:35], v[10:11], s[76:77], v[34:35] op_sel_hi:[0,1,1]
	v_pk_mul_f32 v[36:37], v[34:35], v[30:31] op_sel_hi:[1,0]
	v_pk_mul_f32 v[30:31], v[14:15], s[2:3] op_sel_hi:[0,1] neg_lo:[1,0]
	v_add_f32_e32 v26, v59, v13
	v_pk_fma_f32 v[30:31], v[10:11], s[0:1], v[30:31] op_sel_hi:[0,1,1]
	v_lshlrev_b32_e32 v13, 16, v15
	s_mov_b32 s4, s7
	s_mov_b32 s5, s9
	v_pk_mul_f32 v[34:35], v[14:15], s[6:7] op_sel_hi:[0,1] neg_lo:[1,0]
	v_pk_mul_f32 v[26:27], v[30:31], v[26:27] op_sel_hi:[1,0]
	v_add_f32_e32 v30, v57, v13
	v_pk_fma_f32 v[34:35], v[10:11], s[4:5], v[34:35] op_sel_hi:[0,1,1]
	v_pk_mul_f32 v[98:99], v[34:35], v[30:31] op_sel_hi:[1,0]
	s_waitcnt vmcnt(5)
	v_lshlrev_b32_e32 v13, 16, v23
	s_mov_b32 s8, s11
	s_mov_b32 s9, s13
	v_pk_mul_f32 v[34:35], v[14:15], s[10:11] op_sel_hi:[0,1] neg_lo:[1,0]
	v_add_f32_e32 v30, v55, v13
	v_pk_fma_f32 v[34:35], v[10:11], s[8:9], v[34:35] op_sel_hi:[0,1,1]
	v_pk_mul_f32 v[100:101], v[34:35], v[30:31] op_sel_hi:[1,0]
	s_waitcnt vmcnt(3)
	v_lshlrev_b32_e32 v13, 16, v21
	s_mov_b32 s12, s17
	s_mov_b32 s13, s19
	v_pk_mul_f32 v[34:35], v[14:15], s[16:17] op_sel_hi:[0,1] neg_lo:[1,0]
	v_add_f32_e32 v30, v97, v13
	v_pk_fma_f32 v[34:35], v[10:11], s[12:13], v[34:35] op_sel_hi:[0,1,1]
	v_pk_mul_f32 v[102:103], v[34:35], v[30:31] op_sel_hi:[1,0]
	v_lshlrev_b32_e32 v13, 16, v53
	s_mov_b32 s18, s21
	s_mov_b32 s19, s23
	v_pk_mul_f32 v[34:35], v[14:15], s[20:21] op_sel_hi:[0,1] neg_lo:[1,0]
	v_add_f32_e32 v30, v96, v13
	v_pk_fma_f32 v[34:35], v[10:11], s[18:19], v[34:35] op_sel_hi:[0,1,1]
	s_mov_b32 s24, s83
	v_pk_mul_f32 v[96:97], v[34:35], v[30:31] op_sel_hi:[1,0]
	v_lshlrev_b32_e32 v13, 16, v51
	s_mov_b32 s22, s25
	s_mov_b32 s23, s83
	v_pk_mul_f32 v[34:35], v[14:15], s[24:25] op_sel_hi:[0,1] neg_lo:[1,0]
	v_add_f32_e32 v30, v94, v13
	v_pk_fma_f32 v[34:35], v[10:11], s[22:23], v[34:35] op_sel_hi:[0,1,1]
	s_mov_b32 s28, s29
	s_mov_b32 s29, s75
	v_pk_mul_f32 v[104:105], v[34:35], v[30:31] op_sel_hi:[1,0]
	v_lshlrev_b32_e32 v13, 16, v91
	v_pk_mul_f32 v[34:35], v[14:15], s[28:29] op_sel_hi:[0,1] neg_lo:[1,0]
	v_add_f32_e32 v30, v93, v13
	v_pk_fma_f32 v[34:35], v[10:11], s[26:27], v[34:35] op_sel_hi:[0,1,1]
	v_pk_mul_f32 v[90:91], v[34:35], v[30:31] op_sel_hi:[1,0]
	v_lshlrev_b32_e32 v13, 16, v33
	v_pk_mul_f32 v[34:35], v[14:15], s[38:39] op_sel_hi:[0,0] neg_lo:[1,0]
	s_mov_b32 s38, s39
	v_add_f32_e32 v30, v92, v13
	v_pk_fma_f32 v[34:35], v[10:11], s[38:39], v[34:35] op_sel_hi:[0,0,1] neg_lo:[0,0,1] neg_hi:[0,0,1]
	v_pk_mul_f32 v[92:93], v[34:35], v[30:31] op_sel_hi:[1,0]
	v_pk_mul_f32 v[34:35], v[14:15], s[26:27] op_sel_hi:[0,1] neg_lo:[1,0]
	v_pk_fma_f32 v[34:35], v[10:11], s[28:29], v[34:35] op_sel_hi:[0,1,1]
	v_add_f32_e32 v24, v61, v24
	s_waitcnt vmcnt(2)
	v_lshlrev_b32_e32 v13, 16, v25
	v_add_f32_e32 v30, v95, v13
	v_pk_mul_f32 v[94:95], v[34:35], v[30:31] op_sel_hi:[1,0]
	s_waitcnt vmcnt(1)
	v_lshlrev_b32_e32 v13, 16, v39
	v_pk_mul_f32 v[34:35], v[14:15], s[22:23] op_sel_hi:[0,1] neg_lo:[1,0]
	v_add_f32_e32 v30, v106, v13
	v_pk_fma_f32 v[34:35], v[10:11], s[24:25], v[34:35] op_sel_hi:[0,1,1]
	v_pk_mul_f32 v[106:107], v[34:35], v[30:31] op_sel_hi:[1,0]
	s_waitcnt vmcnt(0)
	v_lshlrev_b32_e32 v13, 16, v40
	v_pk_mul_f32 v[34:35], v[14:15], s[18:19] op_sel_hi:[0,1] neg_lo:[1,0]
	v_add_f32_e32 v30, v108, v13
	v_pk_fma_f32 v[34:35], v[10:11], s[20:21], v[34:35] op_sel_hi:[0,1,1]
	v_pk_mul_f32 v[108:109], v[34:35], v[30:31] op_sel_hi:[1,0]
	v_lshlrev_b32_e32 v13, 16, v110
	v_pk_mul_f32 v[34:35], v[14:15], s[12:13] op_sel_hi:[0,1] neg_lo:[1,0]
	v_add_f32_e32 v30, v111, v13
	v_pk_fma_f32 v[34:35], v[10:11], s[16:17], v[34:35] op_sel_hi:[0,1,1]
	v_pk_mul_f32 v[110:111], v[34:35], v[30:31] op_sel_hi:[1,0]
	v_lshlrev_b32_e32 v13, 16, v112
	v_pk_mul_f32 v[34:35], v[14:15], s[8:9] op_sel_hi:[0,1] neg_lo:[1,0]
	v_add_f32_e32 v30, v113, v13
	v_pk_fma_f32 v[34:35], v[10:11], s[10:11], v[34:35] op_sel_hi:[0,1,1]
	v_pk_mul_f32 v[112:113], v[34:35], v[30:31] op_sel_hi:[1,0]
	v_lshlrev_b32_e32 v13, 16, v114
	v_pk_mul_f32 v[34:35], v[14:15], s[4:5] op_sel_hi:[0,1] neg_lo:[1,0]
	v_add_f32_e32 v30, v115, v13
	v_pk_fma_f32 v[34:35], v[10:11], s[6:7], v[34:35] op_sel_hi:[0,1,1]
	v_lshlrev_b32_e32 v13, 16, v116
	v_pk_mul_f32 v[14:15], v[14:15], s[0:1] op_sel_hi:[0,1] neg_lo:[1,0]
	v_pk_mul_f32 v[114:115], v[34:35], v[30:31] op_sel_hi:[1,0]
	v_add_f32_e32 v30, v17, v13
	v_pk_fma_f32 v[14:15], v[10:11], s[2:3], v[14:15] op_sel_hi:[0,1,1]
	v_pk_mul_f32 v[116:117], v[14:15], v[30:31] op_sel_hi:[1,0]
	v_mov_b32_e32 v13, v174
	v_mov_b32_e32 v14, v180
	v_mov_b32_e32 v15, v181
	v_mov_b32_e32 v10, v164
	v_mov_b32_e32 v30, v166
	v_mov_b32_e32 v10, v168
	v_mov_b32_e32 v34, v170
	v_mov_b32_e32 v17, v172
	s_nop 0
	v_pk_fma_f32 v[126:127], v[18:19], v[16:17], v[36:37] op_sel_hi:[1,0,1]
	v_pk_fma_f32 v[36:37], v[18:19], v[16:17], v[36:37] op_sel_hi:[1,0,1] neg_lo:[0,0,1] neg_hi:[0,0,1]
	v_pk_fma_f32 v[18:19], v[28:29], v[20:21], v[26:27] op_sel_hi:[1,0,1] neg_lo:[0,0,1] neg_hi:[0,0,1]
	v_pk_fma_f32 v[16:17], v[28:29], v[20:21], v[26:27] op_sel_hi:[1,0,1]
	v_xor_b32_e32 v20, 0x80000000, v19
	v_mov_b32_e32 v21, v18
	v_pk_mul_f32 v[20:21], v[20:21], v[124:125] op_sel_hi:[1,0] neg_lo:[0,1] neg_hi:[0,1]
	s_nop 0
	v_pk_fma_f32 v[40:41], v[18:19], v[118:119], v[20:21] op_sel_hi:[1,0,1]
	v_pk_fma_f32 v[20:21], v[46:47], v[22:23], v[98:99] op_sel_hi:[1,0,1] neg_lo:[0,0,1] neg_hi:[0,0,1]
	v_pk_fma_f32 v[18:19], v[46:47], v[22:23], v[98:99] op_sel_hi:[1,0,1]
	v_xor_b32_e32 v22, 0x80000000, v21
	v_mov_b32_e32 v23, v20
	v_pk_mul_f32 v[22:23], v[22:23], v[34:35] op_sel_hi:[1,0] neg_lo:[0,1] neg_hi:[0,1]
	s_nop 0
	v_pk_fma_f32 v[46:47], v[20:21], v[30:31], v[22:23] op_sel_hi:[1,0,1]
	v_pk_fma_f32 v[22:23], v[88:89], v[52:53], v[100:101] op_sel_hi:[1,0,1] neg_lo:[0,0,1] neg_hi:[0,0,1]
	v_pk_fma_f32 v[20:21], v[88:89], v[52:53], v[100:101] op_sel_hi:[1,0,1]
	v_xor_b32_e32 v26, 0x80000000, v23
	v_mov_b32_e32 v27, v22
	v_pk_mul_f32 v[26:27], v[26:27], v[122:123] op_sel_hi:[1,0] neg_lo:[0,1] neg_hi:[0,1]
	s_nop 0
	v_pk_fma_f32 v[52:53], v[22:23], v[120:121], v[26:27] op_sel_hi:[1,0,1]
	v_pk_fma_f32 v[26:27], v[66:67], v[54:55], v[102:103] op_sel_hi:[1,0,1] neg_lo:[0,0,1] neg_hi:[0,0,1]
	v_pk_fma_f32 v[22:23], v[66:67], v[54:55], v[102:103] op_sel_hi:[1,0,1]
	v_xor_b32_e32 v28, 0x80000000, v27
	v_mov_b32_e32 v29, v26
	v_pk_mul_f32 v[28:29], v[28:29], v[10:11] op_sel_hi:[1,0] neg_lo:[0,1] neg_hi:[0,1]
	s_nop 0
	v_pk_fma_f32 v[54:55], v[26:27], v[10:11], v[28:29] op_sel_hi:[1,0,1]
	v_pk_fma_f32 v[28:29], v[64:65], v[32:33], v[96:97] op_sel_hi:[1,0,1] neg_lo:[0,0,1] neg_hi:[0,0,1]
	v_pk_fma_f32 v[26:27], v[64:65], v[32:33], v[96:97] op_sel_hi:[1,0,1]
	v_pk_mul_f32 v[32:33], v[28:29], v[122:123] op_sel_hi:[1,0]
	v_xor_b32_e32 v64, 0x80000000, v29
	v_mov_b32_e32 v65, v28
	v_pk_fma_f32 v[64:65], v[64:65], v[120:121], v[32:33] op_sel_hi:[1,0,1] neg_lo:[0,1,0] neg_hi:[0,1,0]
	v_pk_fma_f32 v[32:33], v[68:69], v[38:39], v[104:105] op_sel_hi:[1,0,1] neg_lo:[0,0,1] neg_hi:[0,0,1]
	v_pk_fma_f32 v[28:29], v[68:69], v[38:39], v[104:105] op_sel_hi:[1,0,1]
	v_pk_mul_f32 v[38:39], v[32:33], v[34:35] op_sel_hi:[1,0]
	v_xor_b32_e32 v66, 0x80000000, v33
	v_mov_b32_e32 v67, v32
	v_pk_fma_f32 v[66:67], v[66:67], v[30:31], v[38:39] op_sel_hi:[1,0,1] neg_lo:[0,1,0] neg_hi:[0,1,0]
	v_pk_fma_f32 v[38:39], v[74:75], v[42:43], v[90:91] op_sel_hi:[1,0,1] neg_lo:[0,0,1] neg_hi:[0,0,1]
	v_pk_fma_f32 v[32:33], v[74:75], v[42:43], v[90:91] op_sel_hi:[1,0,1]
	v_pk_mul_f32 v[42:43], v[38:39], v[124:125] op_sel_hi:[1,0]
	v_xor_b32_e32 v68, 0x80000000, v39
	v_mov_b32_e32 v69, v38
	v_pk_fma_f32 v[68:69], v[68:69], v[118:119], v[42:43] op_sel_hi:[1,0,1] neg_lo:[0,1,0] neg_hi:[0,1,0]
	v_pk_fma_f32 v[38:39], v[76:77], v[48:49], v[92:93] op_sel_hi:[1,0,1]
	v_pk_fma_f32 v[42:43], v[76:77], v[48:49], v[92:93] op_sel_hi:[1,0,1] neg_lo:[0,0,1] neg_hi:[0,0,1]
	v_pk_fma_f32 v[48:49], v[82:83], v[56:57], v[94:95] op_sel_hi:[1,0,1] neg_lo:[0,0,1] neg_hi:[0,0,1]
	v_xor_b32_e32 v75, 0x80000000, v42
	v_mov_b32_e32 v74, v43
	v_pk_fma_f32 v[42:43], v[82:83], v[56:57], v[94:95] op_sel_hi:[1,0,1]
	v_pk_mul_f32 v[56:57], v[48:49], v[124:125] op_sel_hi:[1,0] neg_lo:[0,1] neg_hi:[0,1]
	v_xor_b32_e32 v76, 0x80000000, v49
	v_mov_b32_e32 v77, v48
	v_pk_fma_f32 v[48:49], v[84:85], v[58:59], v[106:107] op_sel_hi:[1,0,1]
	v_pk_fma_f32 v[58:59], v[84:85], v[58:59], v[106:107] op_sel_hi:[1,0,1] neg_lo:[0,0,1] neg_hi:[0,0,1]
	v_pk_fma_f32 v[56:57], v[76:77], v[118:119], v[56:57] op_sel_hi:[1,0,1] neg_lo:[0,1,0] neg_hi:[0,1,0]
	v_pk_mul_f32 v[76:77], v[58:59], v[34:35] op_sel_hi:[1,0] neg_lo:[0,1] neg_hi:[0,1]
	v_xor_b32_e32 v82, 0x80000000, v59
	v_mov_b32_e32 v83, v58
	v_pk_fma_f32 v[58:59], v[82:83], v[30:31], v[76:77] op_sel_hi:[1,0,1] neg_lo:[0,1,0] neg_hi:[0,1,0]
	v_pk_fma_f32 v[76:77], v[86:87], v[60:61], v[108:109] op_sel_hi:[1,0,1]
	v_pk_fma_f32 v[60:61], v[86:87], v[60:61], v[108:109] op_sel_hi:[1,0,1] neg_lo:[0,0,1] neg_hi:[0,0,1]
	s_nop 0
	v_pk_mul_f32 v[82:83], v[60:61], v[122:123] op_sel_hi:[1,0] neg_lo:[0,1] neg_hi:[0,1]
	v_xor_b32_e32 v84, 0x80000000, v61
	v_mov_b32_e32 v85, v60
	v_pk_fma_f32 v[60:61], v[84:85], v[120:121], v[82:83] op_sel_hi:[1,0,1] neg_lo:[0,1,0] neg_hi:[0,1,0]
	v_pk_fma_f32 v[82:83], v[80:81], v[62:63], v[110:111] op_sel_hi:[1,0,1]
	v_pk_fma_f32 v[62:63], v[80:81], v[62:63], v[110:111] op_sel_hi:[1,0,1] neg_lo:[0,0,1] neg_hi:[0,0,1]
	v_pk_add_f32 v[84:85], v[126:127], v[38:39] neg_lo:[0,1] neg_hi:[0,1]
	v_xor_b32_e32 v80, 0x80000000, v63
	v_mov_b32_e32 v81, v62
	v_pk_mul_f32 v[80:81], v[80:81], v[10:11] op_sel_hi:[1,0] neg_lo:[0,1] neg_hi:[0,1]
	s_nop 0
	v_pk_fma_f32 v[62:63], v[62:63], v[10:11], v[80:81] op_sel_hi:[1,0,1] neg_lo:[0,1,0] neg_hi:[0,1,0]
	v_pk_fma_f32 v[80:81], v[78:79], v[50:51], v[112:113] op_sel_hi:[1,0,1]
	v_pk_fma_f32 v[50:51], v[78:79], v[50:51], v[112:113] op_sel_hi:[1,0,1] neg_lo:[0,0,1] neg_hi:[0,0,1]
	s_nop 0
	v_xor_b32_e32 v78, 0x80000000, v51
	v_mov_b32_e32 v79, v50
	v_pk_mul_f32 v[78:79], v[78:79], v[122:123] op_sel_hi:[1,0] neg_lo:[0,1] neg_hi:[0,1]
	s_nop 0
	v_pk_fma_f32 v[50:51], v[50:51], v[120:121], v[78:79] op_sel_hi:[1,0,1] neg_lo:[0,1,0] neg_hi:[0,1,0]
	v_pk_fma_f32 v[78:79], v[70:71], v[24:25], v[114:115] op_sel_hi:[1,0,1]
	v_pk_fma_f32 v[24:25], v[70:71], v[24:25], v[114:115] op_sel_hi:[1,0,1] neg_lo:[0,0,1] neg_hi:[0,0,1]
	s_nop 0
	v_xor_b32_e32 v70, 0x80000000, v25
	v_mov_b32_e32 v71, v24
	v_pk_mul_f32 v[70:71], v[70:71], v[34:35] op_sel_hi:[1,0] neg_lo:[0,1] neg_hi:[0,1]
	s_nop 0
	v_pk_fma_f32 v[70:71], v[24:25], v[30:31], v[70:71] op_sel_hi:[1,0,1] neg_lo:[0,1,0] neg_hi:[0,1,0]
	v_pk_fma_f32 v[24:25], v[72:73], v[44:45], v[116:117] op_sel_hi:[1,0,1]
	v_pk_fma_f32 v[44:45], v[72:73], v[44:45], v[116:117] op_sel_hi:[1,0,1] neg_lo:[0,0,1] neg_hi:[0,0,1]
	s_nop 0
	v_xor_b32_e32 v72, 0x80000000, v45
	v_mov_b32_e32 v73, v44
	v_pk_mul_f32 v[72:73], v[72:73], v[124:125] op_sel_hi:[1,0] neg_lo:[0,1] neg_hi:[0,1]
	s_nop 0
	v_pk_fma_f32 v[72:73], v[118:119], v[44:45], v[72:73] op_sel_hi:[0,1,1] neg_lo:[1,0,0] neg_hi:[1,0,0]
	v_pk_add_f32 v[44:45], v[126:127], v[38:39]
	v_pk_add_f32 v[38:39], v[16:17], v[42:43]
	v_pk_add_f32 v[16:17], v[16:17], v[42:43] neg_lo:[0,1] neg_hi:[0,1]
	s_nop 0
	v_xor_b32_e32 v42, 0x80000000, v17
	v_mov_b32_e32 v43, v16
	v_pk_mul_f32 v[42:43], v[42:43], v[34:35] op_sel_hi:[1,0] neg_lo:[0,1] neg_hi:[0,1]
	s_nop 0
	v_pk_fma_f32 v[42:43], v[16:17], v[30:31], v[42:43] op_sel_hi:[1,0,1]
	v_pk_add_f32 v[16:17], v[18:19], v[48:49]
	v_pk_add_f32 v[18:19], v[18:19], v[48:49] neg_lo:[0,1] neg_hi:[0,1]
	s_nop 0
	v_xor_b32_e32 v48, 0x80000000, v19
	v_mov_b32_e32 v49, v18
	v_pk_mul_f32 v[48:49], v[48:49], v[10:11] op_sel_hi:[1,0] neg_lo:[0,1] neg_hi:[0,1]
	s_nop 0
	v_pk_fma_f32 v[18:19], v[18:19], v[10:11], v[48:49] op_sel_hi:[1,0,1]
	v_pk_add_f32 v[48:49], v[20:21], v[76:77]
	v_pk_add_f32 v[20:21], v[20:21], v[76:77] neg_lo:[0,1] neg_hi:[0,1]
	s_nop 0
	v_pk_mul_f32 v[76:77], v[20:21], v[34:35] op_sel_hi:[1,0]
	v_xor_b32_e32 v86, 0x80000000, v21
	v_mov_b32_e32 v87, v20
	v_pk_add_f32 v[20:21], v[22:23], v[82:83]
	v_pk_add_f32 v[22:23], v[22:23], v[82:83] neg_lo:[0,1] neg_hi:[0,1]
	v_pk_fma_f32 v[76:77], v[86:87], v[30:31], v[76:77] op_sel_hi:[1,0,1] neg_lo:[0,1,0] neg_hi:[0,1,0]
	v_xor_b32_e32 v83, 0x80000000, v22
	v_mov_b32_e32 v82, v23
	v_pk_add_f32 v[22:23], v[26:27], v[80:81]
	v_pk_add_f32 v[26:27], v[26:27], v[80:81] neg_lo:[0,1] neg_hi:[0,1]
	s_nop 0
	v_pk_mul_f32 v[80:81], v[26:27], v[34:35] op_sel_hi:[1,0] neg_lo:[0,1] neg_hi:[0,1]
	v_xor_b32_e32 v86, 0x80000000, v27
	v_mov_b32_e32 v87, v26
	v_pk_fma_f32 v[26:27], v[30:31], v[86:87], v[80:81] op_sel_hi:[0,1,1] neg_lo:[1,0,0] neg_hi:[1,0,0]
	v_pk_add_f32 v[80:81], v[28:29], v[78:79]
	v_pk_add_f32 v[28:29], v[28:29], v[78:79] neg_lo:[0,1] neg_hi:[0,1]
	v_pk_add_f32 v[86:87], v[44:45], v[20:21] neg_lo:[0,1] neg_hi:[0,1]
	v_xor_b32_e32 v78, 0x80000000, v29
	v_mov_b32_e32 v79, v28
	v_pk_mul_f32 v[78:79], v[10:11], v[78:79] op_sel_hi:[0,1] neg_lo:[1,0] neg_hi:[1,0]
	v_pk_fma_f32 v[78:79], v[28:29], v[10:11], v[78:79] op_sel_hi:[1,0,1] neg_lo:[0,1,0] neg_hi:[0,1,0]
	v_pk_add_f32 v[28:29], v[32:33], v[24:25]
	v_pk_add_f32 v[24:25], v[32:33], v[24:25] neg_lo:[0,1] neg_hi:[0,1]
	s_nop 0
	v_xor_b32_e32 v32, 0x80000000, v25
	v_mov_b32_e32 v33, v24
	v_pk_mul_f32 v[32:33], v[34:35], v[32:33] op_sel_hi:[0,1] neg_lo:[1,0] neg_hi:[1,0]
	v_pk_fma_f32 v[32:33], v[30:31], v[24:25], v[32:33] op_sel_hi:[0,1,1] neg_lo:[1,0,0] neg_hi:[1,0,0]
	v_pk_add_f32 v[24:25], v[44:45], v[20:21]
	v_pk_add_f32 v[20:21], v[38:39], v[22:23]
	v_pk_add_f32 v[22:23], v[38:39], v[22:23] neg_lo:[0,1] neg_hi:[0,1]
	s_nop 0
	v_xor_b32_e32 v38, 0x80000000, v23
	v_mov_b32_e32 v39, v22
	v_pk_mul_f32 v[38:39], v[10:11], v[38:39] op_sel_hi:[0,1] neg_lo:[1,0] neg_hi:[1,0]
	v_pk_fma_f32 v[22:23], v[22:23], v[10:11], v[38:39] op_sel_hi:[1,0,1]
	v_pk_add_f32 v[38:39], v[16:17], v[80:81]
	v_pk_add_f32 v[16:17], v[16:17], v[80:81] neg_lo:[0,1] neg_hi:[0,1]
	s_nop 0
	v_xor_b32_e32 v81, 0x80000000, v16
	v_mov_b32_e32 v80, v17
	v_pk_add_f32 v[16:17], v[48:49], v[28:29]
	v_pk_add_f32 v[28:29], v[48:49], v[28:29] neg_lo:[0,1] neg_hi:[0,1]
	s_nop 0
	v_xor_b32_e32 v44, 0x80000000, v29
	v_mov_b32_e32 v45, v28
	v_pk_mul_f32 v[44:45], v[10:11], v[44:45] op_sel_hi:[0,1] neg_lo:[1,0] neg_hi:[1,0]
	v_pk_fma_f32 v[48:49], v[10:11], v[28:29], v[44:45] op_sel_hi:[0,1,1] neg_lo:[1,0,0] neg_hi:[1,0,0]
	v_pk_add_f32 v[28:29], v[24:25], v[38:39]
	v_pk_add_f32 v[24:25], v[24:25], v[38:39] neg_lo:[0,1] neg_hi:[0,1]
	v_pk_add_f32 v[38:39], v[20:21], v[16:17]
	v_pk_add_f32 v[16:17], v[20:21], v[16:17] neg_lo:[0,1] neg_hi:[0,1]
	v_pk_add_f32 v[88:89], v[28:29], v[38:39]
	v_xor_b32_e32 v21, 0x80000000, v16
	v_mov_b32_e32 v20, v17
	v_pk_add_f32 v[44:45], v[24:25], v[20:21]
	v_pk_add_f32 v[20:21], v[24:25], v[20:21] neg_lo:[0,1] neg_hi:[0,1]
	v_pk_add_f32 v[24:25], v[22:23], v[48:49]
	v_pk_add_f32 v[22:23], v[22:23], v[48:49] neg_lo:[0,1] neg_hi:[0,1]
	v_pk_add_f32 v[16:17], v[86:87], v[80:81]
	v_pk_add_f32 v[80:81], v[86:87], v[80:81] neg_lo:[0,1] neg_hi:[0,1]
	v_xor_b32_e32 v49, 0x80000000, v22
	v_mov_b32_e32 v48, v23
	v_pk_add_f32 v[28:29], v[28:29], v[38:39] neg_lo:[0,1] neg_hi:[0,1]
	v_pk_add_f32 v[86:87], v[16:17], v[24:25]
	v_pk_add_f32 v[24:25], v[16:17], v[24:25] neg_lo:[0,1] neg_hi:[0,1]
	v_pk_add_f32 v[38:39], v[80:81], v[48:49]
	v_pk_add_f32 v[16:17], v[80:81], v[48:49] neg_lo:[0,1] neg_hi:[0,1]
	v_pk_add_f32 v[48:49], v[42:43], v[26:27]
	v_pk_add_f32 v[26:27], v[42:43], v[26:27] neg_lo:[0,1] neg_hi:[0,1]
	v_pk_add_f32 v[22:23], v[84:85], v[82:83]
	v_xor_b32_e32 v42, 0x80000000, v27
	v_mov_b32_e32 v43, v26
	v_pk_mul_f32 v[42:43], v[10:11], v[42:43] op_sel_hi:[0,1] neg_lo:[1,0] neg_hi:[1,0]
	v_pk_fma_f32 v[26:27], v[10:11], v[26:27], v[42:43] op_sel_hi:[0,1,1]
	v_pk_add_f32 v[42:43], v[18:19], v[78:79]
	v_pk_add_f32 v[18:19], v[18:19], v[78:79] neg_lo:[0,1] neg_hi:[0,1]
	v_pk_add_f32 v[80:81], v[84:85], v[82:83] neg_lo:[0,1] neg_hi:[0,1]
	v_xor_b32_e32 v79, 0x80000000, v18
	v_mov_b32_e32 v78, v19
	v_pk_add_f32 v[18:19], v[76:77], v[32:33]
	v_pk_add_f32 v[32:33], v[76:77], v[32:33] neg_lo:[0,1] neg_hi:[0,1]
	s_nop 0
	v_xor_b32_e32 v76, 0x80000000, v33
	v_mov_b32_e32 v77, v32
	v_pk_mul_f32 v[76:77], v[10:11], v[76:77] op_sel_hi:[0,1] neg_lo:[1,0] neg_hi:[1,0]
	v_pk_fma_f32 v[76:77], v[10:11], v[32:33], v[76:77] op_sel_hi:[0,1,1] neg_lo:[1,0,0] neg_hi:[1,0,0]
	v_pk_add_f32 v[32:33], v[22:23], v[42:43]
	v_pk_add_f32 v[22:23], v[22:23], v[42:43] neg_lo:[0,1] neg_hi:[0,1]
	v_pk_add_f32 v[42:43], v[48:49], v[18:19]
	v_pk_add_f32 v[18:19], v[48:49], v[18:19] neg_lo:[0,1] neg_hi:[0,1]
	v_pk_add_f32 v[84:85], v[32:33], v[42:43]
	v_pk_add_f32 v[32:33], v[32:33], v[42:43] neg_lo:[0,1] neg_hi:[0,1]
	v_pk_add_f32 v[42:43], v[26:27], v[76:77]
	v_pk_add_f32 v[26:27], v[26:27], v[76:77] neg_lo:[0,1] neg_hi:[0,1]
	v_xor_b32_e32 v83, 0x80000000, v18
	v_mov_b32_e32 v82, v19
	v_pk_add_f32 v[18:19], v[80:81], v[78:79]
	v_pk_add_f32 v[78:79], v[80:81], v[78:79] neg_lo:[0,1] neg_hi:[0,1]
	v_xor_b32_e32 v77, 0x80000000, v26
	v_mov_b32_e32 v76, v27
	v_pk_add_f32 v[80:81], v[18:19], v[42:43]
	v_pk_add_f32 v[26:27], v[18:19], v[42:43] neg_lo:[0,1] neg_hi:[0,1]
	v_pk_add_f32 v[42:43], v[78:79], v[76:77]
	v_pk_add_f32 v[18:19], v[78:79], v[76:77] neg_lo:[0,1] neg_hi:[0,1]
	v_pk_add_f32 v[76:77], v[36:37], v[74:75]
	v_pk_add_f32 v[74:75], v[36:37], v[74:75] neg_lo:[0,1] neg_hi:[0,1]
	v_pk_add_f32 v[36:37], v[40:41], v[56:57]
	v_pk_add_f32 v[40:41], v[40:41], v[56:57] neg_lo:[0,1] neg_hi:[0,1]
	v_pk_add_f32 v[48:49], v[22:23], v[82:83]
	v_xor_b32_e32 v56, 0x80000000, v41
	v_mov_b32_e32 v57, v40
	v_pk_mul_f32 v[56:57], v[34:35], v[56:57] op_sel_hi:[0,1] neg_lo:[1,0] neg_hi:[1,0]
	v_pk_fma_f32 v[40:41], v[30:31], v[40:41], v[56:57] op_sel_hi:[0,1,1]
	v_pk_add_f32 v[56:57], v[46:47], v[58:59]
	v_pk_add_f32 v[46:47], v[46:47], v[58:59] neg_lo:[0,1] neg_hi:[0,1]
	v_pk_add_f32 v[22:23], v[22:23], v[82:83] neg_lo:[0,1] neg_hi:[0,1]
	v_xor_b32_e32 v58, 0x80000000, v47
	v_mov_b32_e32 v59, v46
	v_pk_mul_f32 v[58:59], v[10:11], v[58:59] op_sel_hi:[0,1] neg_lo:[1,0] neg_hi:[1,0]
	v_pk_fma_f32 v[58:59], v[10:11], v[46:47], v[58:59] op_sel_hi:[0,1,1]
	v_pk_add_f32 v[46:47], v[52:53], v[60:61]
	v_pk_add_f32 v[52:53], v[52:53], v[60:61] neg_lo:[0,1] neg_hi:[0,1]
	s_nop 0
	v_xor_b32_e32 v60, 0x80000000, v53
	v_mov_b32_e32 v61, v52
	v_pk_mul_f32 v[60:61], v[30:31], v[60:61] op_sel_hi:[0,1] neg_lo:[1,0] neg_hi:[1,0]
	v_pk_fma_f32 v[60:61], v[34:35], v[52:53], v[60:61] op_sel_hi:[0,1,1]
	v_pk_add_f32 v[52:53], v[54:55], v[62:63]
	v_pk_add_f32 v[54:55], v[54:55], v[62:63] neg_lo:[0,1] neg_hi:[0,1]
	s_nop 0
	v_xor_b32_e32 v63, 0x80000000, v54
	v_mov_b32_e32 v62, v55
	v_pk_add_f32 v[54:55], v[64:65], v[50:51]
	v_pk_add_f32 v[50:51], v[64:65], v[50:51] neg_lo:[0,1] neg_hi:[0,1]
	s_nop 0
	v_xor_b32_e32 v64, 0x80000000, v51
	v_mov_b32_e32 v65, v50
	v_pk_mul_f32 v[64:65], v[30:31], v[64:65] op_sel_hi:[0,1] neg_lo:[1,0] neg_hi:[1,0]
	v_pk_fma_f32 v[50:51], v[34:35], v[50:51], v[64:65] op_sel_hi:[0,1,1] neg_lo:[1,0,0] neg_hi:[1,0,0]
	v_pk_add_f32 v[64:65], v[66:67], v[70:71]
	v_pk_add_f32 v[66:67], v[66:67], v[70:71] neg_lo:[0,1] neg_hi:[0,1]
	s_nop 0
	v_xor_b32_e32 v70, 0x80000000, v67
	v_mov_b32_e32 v71, v66
	v_pk_mul_f32 v[70:71], v[10:11], v[70:71] op_sel_hi:[0,1] neg_lo:[1,0] neg_hi:[1,0]
	v_pk_fma_f32 v[66:67], v[10:11], v[66:67], v[70:71] op_sel_hi:[0,1,1] neg_lo:[1,0,0] neg_hi:[1,0,0]
	v_pk_add_f32 v[70:71], v[68:69], v[72:73]
	v_pk_add_f32 v[68:69], v[68:69], v[72:73] neg_lo:[0,1] neg_hi:[0,1]
	s_nop 0
	v_xor_b32_e32 v72, 0x80000000, v69
	v_mov_b32_e32 v73, v68
	v_pk_mul_f32 v[34:35], v[34:35], v[72:73] op_sel_hi:[0,1] neg_lo:[1,0] neg_hi:[1,0]
	v_pk_fma_f32 v[34:35], v[30:31], v[68:69], v[34:35] op_sel_hi:[0,1,1] neg_lo:[1,0,0] neg_hi:[1,0,0]
	v_pk_add_f32 v[30:31], v[76:77], v[52:53]
	v_pk_add_f32 v[68:69], v[76:77], v[52:53] neg_lo:[0,1] neg_hi:[0,1]
	v_pk_add_f32 v[52:53], v[54:55], v[36:37]
	v_pk_add_f32 v[36:37], v[36:37], v[54:55] neg_lo:[0,1] neg_hi:[0,1]
	s_nop 0
	v_xor_b32_e32 v54, 0x80000000, v37
	v_mov_b32_e32 v55, v36
	v_pk_mul_f32 v[54:55], v[10:11], v[54:55] op_sel_hi:[0,1] neg_lo:[1,0] neg_hi:[1,0]
	v_pk_fma_f32 v[54:55], v[10:11], v[36:37], v[54:55] op_sel_hi:[0,1,1]
	v_pk_add_f32 v[36:37], v[56:57], v[64:65]
	v_pk_add_f32 v[56:57], v[56:57], v[64:65] neg_lo:[0,1] neg_hi:[0,1]
	s_nop 0
	v_xor_b32_e32 v65, 0x80000000, v56
	v_mov_b32_e32 v64, v57
	v_pk_add_f32 v[56:57], v[46:47], v[70:71]
	v_pk_add_f32 v[46:47], v[46:47], v[70:71] neg_lo:[0,1] neg_hi:[0,1]
	s_nop 0
	v_xor_b32_e32 v70, 0x80000000, v47
	v_mov_b32_e32 v71, v46
	v_pk_mul_f32 v[70:71], v[10:11], v[70:71] op_sel_hi:[0,1] neg_lo:[1,0] neg_hi:[1,0]
	v_pk_fma_f32 v[46:47], v[10:11], v[46:47], v[70:71] op_sel_hi:[0,1,1] neg_lo:[1,0,0] neg_hi:[1,0,0]
	v_pk_add_f32 v[70:71], v[30:31], v[36:37]
	v_pk_add_f32 v[30:31], v[30:31], v[36:37] neg_lo:[0,1] neg_hi:[0,1]
	v_pk_add_f32 v[36:37], v[52:53], v[56:57]
	v_pk_add_f32 v[52:53], v[52:53], v[56:57] neg_lo:[0,1] neg_hi:[0,1]
	v_pk_add_f32 v[72:73], v[70:71], v[36:37]
	v_xor_b32_e32 v57, 0x80000000, v52
	v_mov_b32_e32 v56, v53
	v_pk_add_f32 v[52:53], v[70:71], v[36:37] neg_lo:[0,1] neg_hi:[0,1]
	v_pk_add_f32 v[70:71], v[30:31], v[56:57]
	v_pk_add_f32 v[36:37], v[30:31], v[56:57] neg_lo:[0,1] neg_hi:[0,1]
	v_pk_add_f32 v[30:31], v[68:69], v[64:65]
	v_pk_add_f32 v[56:57], v[68:69], v[64:65] neg_lo:[0,1] neg_hi:[0,1]
	v_pk_add_f32 v[64:65], v[54:55], v[46:47]
	v_pk_add_f32 v[46:47], v[54:55], v[46:47] neg_lo:[0,1] neg_hi:[0,1]
	v_pk_add_f32 v[68:69], v[30:31], v[64:65]
	v_xor_b32_e32 v55, 0x80000000, v46
	v_mov_b32_e32 v54, v47
	v_pk_add_f32 v[46:47], v[30:31], v[64:65] neg_lo:[0,1] neg_hi:[0,1]
	v_pk_add_f32 v[64:65], v[56:57], v[54:55]
	v_pk_add_f32 v[30:31], v[56:57], v[54:55] neg_lo:[0,1] neg_hi:[0,1]
	v_pk_add_f32 v[54:55], v[74:75], v[62:63]
	v_pk_add_f32 v[56:57], v[74:75], v[62:63] neg_lo:[0,1] neg_hi:[0,1]
	v_pk_add_f32 v[62:63], v[50:51], v[40:41]
	v_pk_add_f32 v[40:41], v[40:41], v[50:51] neg_lo:[0,1] neg_hi:[0,1]
	s_nop 0
	v_xor_b32_e32 v50, 0x80000000, v41
	v_mov_b32_e32 v51, v40
	v_pk_mul_f32 v[50:51], v[10:11], v[50:51] op_sel_hi:[0,1] neg_lo:[1,0] neg_hi:[1,0]
	v_pk_fma_f32 v[50:51], v[10:11], v[40:41], v[50:51] op_sel_hi:[0,1,1]
	v_pk_add_f32 v[40:41], v[58:59], v[66:67]
	v_pk_add_f32 v[58:59], v[58:59], v[66:67] neg_lo:[0,1] neg_hi:[0,1]
	s_nop 0
	v_xor_b32_e32 v67, 0x80000000, v58
	v_mov_b32_e32 v66, v59
	v_pk_add_f32 v[58:59], v[60:61], v[34:35]
	v_pk_add_f32 v[34:35], v[60:61], v[34:35] neg_lo:[0,1] neg_hi:[0,1]
	s_nop 0
	v_xor_b32_e32 v60, 0x80000000, v35
	v_mov_b32_e32 v61, v34
	v_pk_mul_f32 v[60:61], v[10:11], v[60:61] op_sel_hi:[0,1] neg_lo:[1,0] neg_hi:[1,0]
	v_pk_fma_f32 v[34:35], v[10:11], v[34:35], v[60:61] op_sel_hi:[0,1,1] neg_lo:[1,0,0] neg_hi:[1,0,0]
	v_pk_add_f32 v[60:61], v[54:55], v[40:41]
	v_pk_add_f32 v[40:41], v[54:55], v[40:41] neg_lo:[0,1] neg_hi:[0,1]
	v_pk_add_f32 v[54:55], v[62:63], v[58:59]
	v_pk_add_f32 v[58:59], v[62:63], v[58:59] neg_lo:[0,1] neg_hi:[0,1]
	v_lshl_add_u32 v10, v13, 3, 0
	v_xor_b32_e32 v63, 0x80000000, v58
	v_mov_b32_e32 v62, v59
	v_pk_add_f32 v[58:59], v[60:61], v[54:55]
	v_pk_add_f32 v[54:55], v[60:61], v[54:55] neg_lo:[0,1] neg_hi:[0,1]
	v_pk_add_f32 v[60:61], v[40:41], v[62:63]
	v_pk_add_f32 v[40:41], v[40:41], v[62:63] neg_lo:[0,1] neg_hi:[0,1]
	v_pk_add_f32 v[62:63], v[56:57], v[66:67]
	v_pk_add_f32 v[56:57], v[56:57], v[66:67] neg_lo:[0,1] neg_hi:[0,1]
	v_pk_add_f32 v[66:67], v[50:51], v[34:35]
	v_pk_add_f32 v[34:35], v[50:51], v[34:35] neg_lo:[0,1] neg_hi:[0,1]
	v_pk_add_f32 v[76:77], v[62:63], v[66:67]
	v_xor_b32_e32 v75, 0x80000000, v34
	v_mov_b32_e32 v74, v35
	v_pk_add_f32 v[50:51], v[62:63], v[66:67] neg_lo:[0,1] neg_hi:[0,1]
	v_pk_add_f32 v[62:63], v[56:57], v[74:75]
	v_pk_add_f32 v[34:35], v[56:57], v[74:75] neg_lo:[0,1] neg_hi:[0,1]
	v_xor_b32_e32 v56, 0x80000000, v89
	v_mov_b32_e32 v57, v89
	v_pk_mul_f32 v[56:57], v[56:57], s[14:15]
	v_xor_b32_e32 v66, 0x80000000, v73
	v_pk_fma_f32 v[56:57], v[88:89], s[42:43], v[56:57] op_sel_hi:[0,1,1]
	ds_write_b64 v10, v[56:57]
	v_pk_fma_f32 v[56:57], v[14:15], s[92:93], v[14:15] op_sel:[1,0,0] op_sel_hi:[0,1,1]
	v_mov_b32_e32 v67, v73
	v_pk_mul_f32 v[66:67], v[56:57], v[66:67] op_sel:[1,0] op_sel_hi:[0,1]
	v_pk_fma_f32 v[66:67], v[56:57], v[72:73], v[66:67] op_sel_hi:[1,0,1]
	ds_write_b64 v10, v[66:67] offset:4224
	v_xor_b32_e32 v66, 0x80000000, v57
	v_mov_b32_e32 v67, v57
	v_pk_mul_f32 v[66:67], v[14:15], v[66:67] op_sel:[1,0] op_sel_hi:[0,1]
	v_pk_fma_f32 v[56:57], v[14:15], v[56:57], v[66:67] op_sel_hi:[1,0,1]
	v_xor_b32_e32 v66, 0x80000000, v85
	v_mov_b32_e32 v67, v85
	v_pk_mul_f32 v[66:67], v[56:57], v[66:67] op_sel:[1,0] op_sel_hi:[0,1]
	v_pk_fma_f32 v[66:67], v[56:57], v[84:85], v[66:67] op_sel_hi:[1,0,1]
	ds_write_b64 v10, v[66:67] offset:8448
	v_xor_b32_e32 v66, 0x80000000, v57
	v_mov_b32_e32 v67, v57
	v_pk_mul_f32 v[66:67], v[14:15], v[66:67] op_sel:[1,0] op_sel_hi:[0,1]
	v_pk_fma_f32 v[56:57], v[14:15], v[56:57], v[66:67] op_sel_hi:[1,0,1]
	v_xor_b32_e32 v66, 0x80000000, v59
	v_mov_b32_e32 v67, v59
	v_pk_mul_f32 v[66:67], v[56:57], v[66:67] op_sel:[1,0] op_sel_hi:[0,1]
	v_pk_fma_f32 v[58:59], v[56:57], v[58:59], v[66:67] op_sel_hi:[1,0,1]
	ds_write_b64 v10, v[58:59] offset:12672
	v_xor_b32_e32 v58, 0x80000000, v57
	v_mov_b32_e32 v59, v57
	v_pk_mul_f32 v[58:59], v[14:15], v[58:59] op_sel:[1,0] op_sel_hi:[0,1]
	v_pk_fma_f32 v[56:57], v[14:15], v[56:57], v[58:59] op_sel_hi:[1,0,1]
	v_xor_b32_e32 v58, 0x80000000, v87
	v_mov_b32_e32 v59, v87
	v_pk_mul_f32 v[58:59], v[56:57], v[58:59] op_sel:[1,0] op_sel_hi:[0,1]
	v_pk_fma_f32 v[58:59], v[56:57], v[86:87], v[58:59] op_sel_hi:[1,0,1]
	ds_write_b64 v10, v[58:59] offset:16896
	v_xor_b32_e32 v58, 0x80000000, v57
	v_mov_b32_e32 v59, v57
	v_pk_mul_f32 v[58:59], v[14:15], v[58:59] op_sel:[1,0] op_sel_hi:[0,1]
	v_pk_fma_f32 v[56:57], v[14:15], v[56:57], v[58:59] op_sel_hi:[1,0,1]
	v_xor_b32_e32 v58, 0x80000000, v69
	v_mov_b32_e32 v59, v69
	v_pk_mul_f32 v[58:59], v[56:57], v[58:59] op_sel:[1,0] op_sel_hi:[0,1]
	v_pk_fma_f32 v[58:59], v[56:57], v[68:69], v[58:59] op_sel_hi:[1,0,1]
	ds_write_b64 v10, v[58:59] offset:21120
	v_xor_b32_e32 v58, 0x80000000, v57
	v_mov_b32_e32 v59, v57
	v_pk_mul_f32 v[58:59], v[14:15], v[58:59] op_sel:[1,0] op_sel_hi:[0,1]
	v_pk_fma_f32 v[56:57], v[14:15], v[56:57], v[58:59] op_sel_hi:[1,0,1]
	v_xor_b32_e32 v58, 0x80000000, v81
	v_mov_b32_e32 v59, v81
	v_pk_mul_f32 v[58:59], v[58:59], v[56:57] op_sel:[0,1] op_sel_hi:[1,0]
	s_nop 0
	v_pk_fma_f32 v[58:59], v[80:81], v[56:57], v[58:59] op_sel_hi:[0,1,1]
	ds_write_b64 v10, v[58:59] offset:25344
	v_xor_b32_e32 v58, 0x80000000, v57
	v_mov_b32_e32 v59, v57
	v_pk_mul_f32 v[58:59], v[14:15], v[58:59] op_sel:[1,0] op_sel_hi:[0,1]
	v_pk_fma_f32 v[56:57], v[14:15], v[56:57], v[58:59] op_sel_hi:[1,0,1]
	v_xor_b32_e32 v58, 0x80000000, v77
	v_mov_b32_e32 v59, v77
	v_pk_mul_f32 v[58:59], v[58:59], v[56:57] op_sel:[0,1] op_sel_hi:[1,0]
	s_nop 0
	v_pk_fma_f32 v[58:59], v[76:77], v[56:57], v[58:59] op_sel_hi:[0,1,1]
	ds_write_b64 v10, v[58:59] offset:29568
	v_xor_b32_e32 v58, 0x80000000, v57
	v_mov_b32_e32 v59, v57
	v_pk_mul_f32 v[58:59], v[14:15], v[58:59] op_sel:[1,0] op_sel_hi:[0,1]
	v_pk_fma_f32 v[56:57], v[14:15], v[56:57], v[58:59] op_sel_hi:[1,0,1]
	v_xor_b32_e32 v58, 0x80000000, v45
	v_mov_b32_e32 v59, v45
	v_pk_mul_f32 v[58:59], v[58:59], v[56:57] op_sel:[0,1] op_sel_hi:[1,0]
	s_nop 0
	v_pk_fma_f32 v[44:45], v[44:45], v[56:57], v[58:59] op_sel_hi:[0,1,1]
	ds_write_b64 v10, v[44:45] offset:33792
	v_xor_b32_e32 v44, 0x80000000, v57
	v_mov_b32_e32 v45, v57
	v_pk_mul_f32 v[44:45], v[14:15], v[44:45] op_sel:[1,0] op_sel_hi:[0,1]
	v_pk_fma_f32 v[44:45], v[14:15], v[56:57], v[44:45] op_sel_hi:[1,0,1]
	v_xor_b32_e32 v56, 0x80000000, v71
	v_mov_b32_e32 v57, v71
	v_pk_mul_f32 v[56:57], v[56:57], v[44:45] op_sel:[0,1] op_sel_hi:[1,0]
	s_nop 0
	v_pk_fma_f32 v[56:57], v[70:71], v[44:45], v[56:57] op_sel_hi:[0,1,1]
	ds_write_b64 v10, v[56:57] offset:38016
	v_xor_b32_e32 v56, 0x80000000, v45
	v_mov_b32_e32 v57, v45
	v_pk_mul_f32 v[56:57], v[14:15], v[56:57] op_sel:[1,0] op_sel_hi:[0,1]
	v_pk_fma_f32 v[44:45], v[14:15], v[44:45], v[56:57] op_sel_hi:[1,0,1]
	v_xor_b32_e32 v56, 0x80000000, v49
	v_mov_b32_e32 v57, v49
	v_pk_mul_f32 v[56:57], v[56:57], v[44:45] op_sel:[0,1] op_sel_hi:[1,0]
	s_nop 0
	v_pk_fma_f32 v[48:49], v[48:49], v[44:45], v[56:57] op_sel_hi:[0,1,1]
	ds_write_b64 v10, v[48:49] offset:42240
	v_xor_b32_e32 v48, 0x80000000, v45
	v_mov_b32_e32 v49, v45
	v_pk_mul_f32 v[48:49], v[14:15], v[48:49] op_sel:[1,0] op_sel_hi:[0,1]
	v_pk_fma_f32 v[44:45], v[14:15], v[44:45], v[48:49] op_sel_hi:[1,0,1]
	v_xor_b32_e32 v48, 0x80000000, v61
	v_mov_b32_e32 v49, v61
	v_pk_mul_f32 v[48:49], v[48:49], v[44:45] op_sel:[0,1] op_sel_hi:[1,0]
	s_nop 0
	v_pk_fma_f32 v[48:49], v[60:61], v[44:45], v[48:49] op_sel_hi:[0,1,1]
	ds_write_b64 v10, v[48:49] offset:46464
	v_xor_b32_e32 v48, 0x80000000, v45
	v_mov_b32_e32 v49, v45
	v_pk_mul_f32 v[48:49], v[14:15], v[48:49] op_sel:[1,0] op_sel_hi:[0,1]
	v_pk_fma_f32 v[44:45], v[14:15], v[44:45], v[48:49] op_sel_hi:[1,0,1]
	v_xor_b32_e32 v48, 0x80000000, v39
	v_mov_b32_e32 v49, v39
	v_pk_mul_f32 v[48:49], v[48:49], v[44:45] op_sel:[0,1] op_sel_hi:[1,0]
	s_nop 0
	v_pk_fma_f32 v[38:39], v[38:39], v[44:45], v[48:49] op_sel_hi:[0,1,1]
	ds_write_b64 v10, v[38:39] offset:50688
	v_xor_b32_e32 v38, 0x80000000, v45
	v_mov_b32_e32 v39, v45
	v_pk_mul_f32 v[38:39], v[14:15], v[38:39] op_sel:[1,0] op_sel_hi:[0,1]
	v_pk_fma_f32 v[38:39], v[14:15], v[44:45], v[38:39] op_sel_hi:[1,0,1]
	v_xor_b32_e32 v44, 0x80000000, v65
	v_mov_b32_e32 v45, v65
	v_pk_mul_f32 v[44:45], v[44:45], v[38:39] op_sel:[0,1] op_sel_hi:[1,0]
	s_nop 0
	v_pk_fma_f32 v[44:45], v[64:65], v[38:39], v[44:45] op_sel_hi:[0,1,1]
	ds_write_b64 v10, v[44:45] offset:54912
	v_xor_b32_e32 v44, 0x80000000, v39
	v_mov_b32_e32 v45, v39
	v_pk_mul_f32 v[44:45], v[14:15], v[44:45] op_sel:[1,0] op_sel_hi:[0,1]
	v_pk_fma_f32 v[38:39], v[14:15], v[38:39], v[44:45] op_sel_hi:[1,0,1]
	v_xor_b32_e32 v44, 0x80000000, v43
	v_mov_b32_e32 v45, v43
	v_pk_mul_f32 v[44:45], v[44:45], v[38:39] op_sel:[0,1] op_sel_hi:[1,0]
	s_nop 0
	v_pk_fma_f32 v[42:43], v[42:43], v[38:39], v[44:45] op_sel_hi:[0,1,1]
	ds_write_b64 v10, v[42:43] offset:59136
	v_xor_b32_e32 v42, 0x80000000, v39
	v_mov_b32_e32 v43, v39
	v_pk_mul_f32 v[42:43], v[14:15], v[42:43] op_sel:[1,0] op_sel_hi:[0,1]
	v_pk_fma_f32 v[38:39], v[14:15], v[38:39], v[42:43] op_sel_hi:[1,0,1]
	v_xor_b32_e32 v42, 0x80000000, v63
	v_mov_b32_e32 v43, v63
	v_pk_mul_f32 v[42:43], v[42:43], v[38:39] op_sel:[0,1] op_sel_hi:[1,0]
	s_nop 0
	v_pk_fma_f32 v[42:43], v[62:63], v[38:39], v[42:43] op_sel_hi:[0,1,1]
	ds_write_b64 v10, v[42:43] offset:63360
	v_xor_b32_e32 v42, 0x80000000, v39
	v_mov_b32_e32 v43, v39
	v_pk_mul_f32 v[42:43], v[14:15], v[42:43] op_sel:[1,0] op_sel_hi:[0,1]
	v_pk_fma_f32 v[38:39], v[14:15], v[38:39], v[42:43] op_sel_hi:[1,0,1]
	v_xor_b32_e32 v42, 0x80000000, v29
	v_mov_b32_e32 v43, v29
	v_pk_mul_f32 v[42:43], v[42:43], v[38:39] op_sel:[0,1] op_sel_hi:[1,0]
	v_add_u32_e32 v13, 0x10800, v10
	v_pk_fma_f32 v[28:29], v[28:29], v[38:39], v[42:43] op_sel_hi:[0,1,1]
	ds_write_b64 v13, v[28:29]
	v_xor_b32_e32 v28, 0x80000000, v39
	v_mov_b32_e32 v29, v39
	v_pk_mul_f32 v[28:29], v[14:15], v[28:29] op_sel:[1,0] op_sel_hi:[0,1]
	v_pk_fma_f32 v[28:29], v[14:15], v[38:39], v[28:29] op_sel_hi:[1,0,1]
	v_xor_b32_e32 v38, 0x80000000, v53
	v_mov_b32_e32 v39, v53
	v_pk_mul_f32 v[38:39], v[38:39], v[28:29] op_sel:[0,1] op_sel_hi:[1,0]
	v_add_u32_e32 v13, 0x11880, v10
	v_pk_fma_f32 v[38:39], v[52:53], v[28:29], v[38:39] op_sel_hi:[0,1,1]
	ds_write_b64 v13, v[38:39]
	v_xor_b32_e32 v38, 0x80000000, v29
	v_mov_b32_e32 v39, v29
	v_pk_mul_f32 v[38:39], v[14:15], v[38:39] op_sel:[1,0] op_sel_hi:[0,1]
	v_pk_fma_f32 v[28:29], v[14:15], v[28:29], v[38:39] op_sel_hi:[1,0,1]
	v_xor_b32_e32 v38, 0x80000000, v33
	v_mov_b32_e32 v39, v33
	v_pk_mul_f32 v[38:39], v[38:39], v[28:29] op_sel:[0,1] op_sel_hi:[1,0]
	v_add_u32_e32 v13, 0x12900, v10
	v_pk_fma_f32 v[32:33], v[32:33], v[28:29], v[38:39] op_sel_hi:[0,1,1]
	ds_write_b64 v13, v[32:33]
	v_xor_b32_e32 v32, 0x80000000, v29
	v_mov_b32_e32 v33, v29
	v_pk_mul_f32 v[32:33], v[14:15], v[32:33] op_sel:[1,0] op_sel_hi:[0,1]
	v_pk_fma_f32 v[28:29], v[14:15], v[28:29], v[32:33] op_sel_hi:[1,0,1]
	v_xor_b32_e32 v32, 0x80000000, v55
	v_mov_b32_e32 v33, v55
	v_pk_mul_f32 v[32:33], v[32:33], v[28:29] op_sel:[0,1] op_sel_hi:[1,0]
	v_add_u32_e32 v13, 0x13980, v10
	v_pk_fma_f32 v[32:33], v[54:55], v[28:29], v[32:33] op_sel_hi:[0,1,1]
	ds_write_b64 v13, v[32:33]
	v_xor_b32_e32 v32, 0x80000000, v29
	v_mov_b32_e32 v33, v29
	v_pk_mul_f32 v[32:33], v[14:15], v[32:33] op_sel:[1,0] op_sel_hi:[0,1]
	v_pk_fma_f32 v[28:29], v[14:15], v[28:29], v[32:33] op_sel_hi:[1,0,1]
	v_xor_b32_e32 v32, 0x80000000, v25
	v_mov_b32_e32 v33, v25
	v_pk_mul_f32 v[32:33], v[32:33], v[28:29] op_sel:[0,1] op_sel_hi:[1,0]
	v_add_u32_e32 v13, 0x14a00, v10
	v_pk_fma_f32 v[24:25], v[24:25], v[28:29], v[32:33] op_sel_hi:[0,1,1]
	ds_write_b64 v13, v[24:25]
	v_xor_b32_e32 v24, 0x80000000, v29
	v_mov_b32_e32 v25, v29
	v_pk_mul_f32 v[24:25], v[14:15], v[24:25] op_sel:[1,0] op_sel_hi:[0,1]
	v_pk_fma_f32 v[24:25], v[14:15], v[28:29], v[24:25] op_sel_hi:[1,0,1]
	v_xor_b32_e32 v28, 0x80000000, v47
	v_mov_b32_e32 v29, v47
	v_pk_mul_f32 v[28:29], v[28:29], v[24:25] op_sel:[0,1] op_sel_hi:[1,0]
	v_add_u32_e32 v13, 0x15a80, v10
	v_pk_fma_f32 v[28:29], v[46:47], v[24:25], v[28:29] op_sel_hi:[0,1,1]
	ds_write_b64 v13, v[28:29]
	v_xor_b32_e32 v28, 0x80000000, v25
	v_mov_b32_e32 v29, v25
	v_pk_mul_f32 v[28:29], v[14:15], v[28:29] op_sel:[1,0] op_sel_hi:[0,1]
	v_pk_fma_f32 v[24:25], v[14:15], v[24:25], v[28:29] op_sel_hi:[1,0,1]
	v_xor_b32_e32 v28, 0x80000000, v27
	v_mov_b32_e32 v29, v27
	v_pk_mul_f32 v[28:29], v[28:29], v[24:25] op_sel:[0,1] op_sel_hi:[1,0]
	v_add_u32_e32 v13, 0x16b00, v10
	v_pk_fma_f32 v[26:27], v[26:27], v[24:25], v[28:29] op_sel_hi:[0,1,1]
	ds_write_b64 v13, v[26:27]
	v_xor_b32_e32 v26, 0x80000000, v25
	v_mov_b32_e32 v27, v25
	v_pk_mul_f32 v[26:27], v[14:15], v[26:27] op_sel:[1,0] op_sel_hi:[0,1]
	v_pk_fma_f32 v[24:25], v[14:15], v[24:25], v[26:27] op_sel_hi:[1,0,1]
	v_xor_b32_e32 v26, 0x80000000, v51
	v_mov_b32_e32 v27, v51
	v_pk_mul_f32 v[26:27], v[26:27], v[24:25] op_sel:[0,1] op_sel_hi:[1,0]
	v_add_u32_e32 v13, 0x17b80, v10
	v_pk_fma_f32 v[26:27], v[50:51], v[24:25], v[26:27] op_sel_hi:[0,1,1]
	ds_write_b64 v13, v[26:27]
	v_xor_b32_e32 v26, 0x80000000, v25
	v_mov_b32_e32 v27, v25
	v_pk_mul_f32 v[26:27], v[14:15], v[26:27] op_sel:[1,0] op_sel_hi:[0,1]
	v_pk_fma_f32 v[24:25], v[14:15], v[24:25], v[26:27] op_sel_hi:[1,0,1]
	v_xor_b32_e32 v26, 0x80000000, v21
	v_mov_b32_e32 v27, v21
	v_pk_mul_f32 v[26:27], v[26:27], v[24:25] op_sel:[0,1] op_sel_hi:[1,0]
	v_add_u32_e32 v13, 0x18c00, v10
	v_pk_fma_f32 v[20:21], v[20:21], v[24:25], v[26:27] op_sel_hi:[0,1,1]
	ds_write_b64 v13, v[20:21]
	v_xor_b32_e32 v20, 0x80000000, v25
	v_mov_b32_e32 v21, v25
	v_pk_mul_f32 v[20:21], v[14:15], v[20:21] op_sel:[1,0] op_sel_hi:[0,1]
	v_pk_fma_f32 v[20:21], v[14:15], v[24:25], v[20:21] op_sel_hi:[1,0,1]
	v_xor_b32_e32 v24, 0x80000000, v37
	v_mov_b32_e32 v25, v37
	v_pk_mul_f32 v[24:25], v[24:25], v[20:21] op_sel:[0,1] op_sel_hi:[1,0]
	v_add_u32_e32 v13, 0x19c80, v10
	v_pk_fma_f32 v[24:25], v[36:37], v[20:21], v[24:25] op_sel_hi:[0,1,1]
	ds_write_b64 v13, v[24:25]
	v_xor_b32_e32 v24, 0x80000000, v21
	v_mov_b32_e32 v25, v21
	v_pk_mul_f32 v[24:25], v[14:15], v[24:25] op_sel:[1,0] op_sel_hi:[0,1]
	v_pk_fma_f32 v[20:21], v[14:15], v[20:21], v[24:25] op_sel_hi:[1,0,1]
	v_xor_b32_e32 v24, 0x80000000, v23
	v_mov_b32_e32 v25, v23
	v_pk_mul_f32 v[24:25], v[24:25], v[20:21] op_sel:[0,1] op_sel_hi:[1,0]
	v_add_u32_e32 v13, 0x1ad00, v10
	v_pk_fma_f32 v[22:23], v[22:23], v[20:21], v[24:25] op_sel_hi:[0,1,1]
	ds_write_b64 v13, v[22:23]
	v_xor_b32_e32 v22, 0x80000000, v21
	v_mov_b32_e32 v23, v21
	v_pk_mul_f32 v[22:23], v[14:15], v[22:23] op_sel:[1,0] op_sel_hi:[0,1]
	v_pk_fma_f32 v[20:21], v[14:15], v[20:21], v[22:23] op_sel_hi:[1,0,1]
	v_xor_b32_e32 v22, 0x80000000, v41
	v_mov_b32_e32 v23, v41
	v_pk_mul_f32 v[22:23], v[22:23], v[20:21] op_sel:[0,1] op_sel_hi:[1,0]
	v_add_u32_e32 v13, 0x1bd80, v10
	v_pk_fma_f32 v[22:23], v[40:41], v[20:21], v[22:23] op_sel_hi:[0,1,1]
	ds_write_b64 v13, v[22:23]
	v_xor_b32_e32 v22, 0x80000000, v21
	v_mov_b32_e32 v23, v21
	v_pk_mul_f32 v[22:23], v[14:15], v[22:23] op_sel:[1,0] op_sel_hi:[0,1]
	v_pk_fma_f32 v[20:21], v[14:15], v[20:21], v[22:23] op_sel_hi:[1,0,1]
	v_xor_b32_e32 v22, 0x80000000, v17
	v_mov_b32_e32 v23, v17
	v_pk_mul_f32 v[22:23], v[22:23], v[20:21] op_sel:[0,1] op_sel_hi:[1,0]
	v_add_u32_e32 v13, 0x1ce00, v10
	v_pk_fma_f32 v[16:17], v[16:17], v[20:21], v[22:23] op_sel_hi:[0,1,1]
	ds_write_b64 v13, v[16:17]
	v_xor_b32_e32 v16, 0x80000000, v21
	v_mov_b32_e32 v17, v21
	v_pk_mul_f32 v[16:17], v[14:15], v[16:17] op_sel:[1,0] op_sel_hi:[0,1]
	v_pk_fma_f32 v[16:17], v[14:15], v[20:21], v[16:17] op_sel_hi:[1,0,1]
	v_xor_b32_e32 v20, 0x80000000, v31
	v_mov_b32_e32 v21, v31
	v_pk_mul_f32 v[20:21], v[20:21], v[16:17] op_sel:[0,1] op_sel_hi:[1,0]
	v_add_u32_e32 v13, 0x1de80, v10
	v_pk_fma_f32 v[20:21], v[30:31], v[16:17], v[20:21] op_sel_hi:[0,1,1]
	ds_write_b64 v13, v[20:21]
	v_xor_b32_e32 v20, 0x80000000, v17
	v_mov_b32_e32 v21, v17
	v_pk_mul_f32 v[20:21], v[14:15], v[20:21] op_sel:[1,0] op_sel_hi:[0,1]
	v_pk_fma_f32 v[16:17], v[14:15], v[16:17], v[20:21] op_sel_hi:[1,0,1]
	v_xor_b32_e32 v20, 0x80000000, v19
	v_mov_b32_e32 v21, v19
	v_pk_mul_f32 v[20:21], v[20:21], v[16:17] op_sel:[0,1] op_sel_hi:[1,0]
	v_add_u32_e32 v13, 0x1ef00, v10
	v_pk_fma_f32 v[18:19], v[18:19], v[16:17], v[20:21] op_sel_hi:[0,1,1]
	ds_write_b64 v13, v[18:19]
	v_xor_b32_e32 v18, 0x80000000, v17
	v_mov_b32_e32 v19, v17
	v_pk_mul_f32 v[18:19], v[14:15], v[18:19] op_sel:[1,0] op_sel_hi:[0,1]
	v_pk_fma_f32 v[14:15], v[14:15], v[16:17], v[18:19] op_sel_hi:[1,0,1]
	v_xor_b32_e32 v16, 0x80000000, v35
	v_mov_b32_e32 v17, v35
	v_pk_mul_f32 v[16:17], v[16:17], v[14:15] op_sel:[0,1] op_sel_hi:[1,0]
	v_add_u32_e32 v10, 0x1ff80, v10
	v_pk_fma_f32 v[14:15], v[34:35], v[14:15], v[16:17] op_sel_hi:[0,1,1]
	ds_write_b64 v10, v[14:15]
	v_mov_b32_e32 v10, v176
	v_mov_b32_e32 v13, v173
	s_waitcnt lgkmcnt(0)
	s_barrier
	v_mov_b32_e32 v14, v182
	v_xad_u32 v28, v13, 3, v10
	v_lshl_add_u32 v71, v28, 3, 0
	v_xad_u32 v28, v13, 4, v10
	v_lshl_add_u32 v70, v28, 3, 0
	v_xad_u32 v28, v13, 5, v10
	v_lshl_add_u32 v69, v28, 3, 0
	v_xad_u32 v28, v13, 6, v10
	v_lshl_add_u32 v68, v28, 3, 0
	v_xad_u32 v28, v13, 7, v10
	v_lshl_add_u32 v67, v28, 3, 0
	v_xad_u32 v28, v13, 8, v10
	v_lshl_add_u32 v28, v28, 3, 0
	v_add_u32_e32 v66, 0x800, v28
	v_xad_u32 v28, v13, 9, v10
	v_lshl_add_u32 v28, v28, 3, 0
	v_add_u32_e32 v65, 0x800, v28
	v_xad_u32 v28, v13, 10, v10
	v_lshl_add_u32 v28, v28, 3, 0
	v_add_u32_e32 v64, 0x800, v28
	v_xad_u32 v28, v13, 11, v10
	v_lshl_add_u32 v28, v28, 3, 0
	v_add_u32_e32 v16, v13, v10
	v_add_u32_e32 v63, 0x800, v28
	v_xad_u32 v28, v13, 12, v10
	v_mov_b32_e32 v15, v183
	v_lshl_add_u32 v74, v16, 3, 0
	v_lshl_add_u32 v28, v28, 3, 0
	ds_read2_b64 v[16:19], v74 offset1:16
	ds_read2_b64 v[38:41], v66 offset1:16
	v_add_u32_e32 v62, 0x800, v28
	v_xad_u32 v28, v13, 13, v10
	v_xad_u32 v20, v13, 1, v10
	v_lshl_add_u32 v28, v28, 3, 0
	v_lshl_add_u32 v73, v20, 3, 0
	v_xad_u32 v24, v13, 2, v10
	v_add_u32_e32 v61, 0x800, v28
	v_xad_u32 v28, v13, 14, v10
	v_xad_u32 v10, v13, 15, v10
	ds_read2_b64 v[20:23], v73 offset0:32 offset1:48
	ds_read2_b64 v[46:49], v65 offset0:32 offset1:48
	v_lshl_add_u32 v28, v28, 3, 0
	v_lshl_add_u32 v10, v10, 3, 0
	v_lshl_add_u32 v72, v24, 3, 0
	v_add_u32_e32 v60, 0x800, v28
	v_add_u32_e32 v13, 0x800, v10
	v_mov_b32_e32 v10, v164
	ds_read2_b64 v[24:27], v72 offset0:64 offset1:80
	ds_read2_b64 v[56:59], v71 offset0:96 offset1:112
	ds_read2_b64 v[76:79], v70 offset0:128 offset1:144
	ds_read2_b64 v[80:83], v69 offset0:160 offset1:176
	ds_read2_b64 v[84:87], v68 offset0:192 offset1:208
	ds_read2_b64 v[88:91], v67 offset0:224 offset1:240
	ds_read2_b64 v[52:55], v64 offset0:64 offset1:80
	ds_read2_b64 v[92:95], v63 offset0:96 offset1:112
	ds_read2_b64 v[96:99], v62 offset0:128 offset1:144
	ds_read2_b64 v[100:103], v61 offset0:160 offset1:176
	ds_read2_b64 v[104:107], v60 offset0:192 offset1:208
	ds_read2_b64 v[108:111], v13 offset0:224 offset1:240
	s_waitcnt lgkmcnt(14)
	v_pk_add_f32 v[112:113], v[16:17], v[38:39]
	v_pk_add_f32 v[38:39], v[16:17], v[38:39] neg_lo:[0,1] neg_hi:[0,1]
	v_pk_add_f32 v[16:17], v[18:19], v[40:41]
	v_pk_add_f32 v[18:19], v[18:19], v[40:41] neg_lo:[0,1] neg_hi:[0,1]
	v_mov_b32_e32 v28, v165
	v_mov_b32_e32 v30, v166
	v_mov_b32_e32 v32, v167
	v_mov_b32_e32 v10, v168
	v_mov_b32_e32 v36, v169
	v_mov_b32_e32 v34, v170
	v_mov_b32_e32 v44, v171
	v_xor_b32_e32 v40, 0x80000000, v19
	v_mov_b32_e32 v41, v18
	v_mov_b32_e32 v29, v172
	v_pk_mul_f32 v[40:41], v[40:41], v[44:45] op_sel_hi:[1,0] neg_lo:[0,1] neg_hi:[0,1]
	s_nop 0
	v_pk_fma_f32 v[42:43], v[18:19], v[28:29], v[40:41] op_sel_hi:[1,0,1]
	s_waitcnt lgkmcnt(12)
	v_pk_add_f32 v[18:19], v[20:21], v[46:47]
	v_pk_add_f32 v[20:21], v[20:21], v[46:47] neg_lo:[0,1] neg_hi:[0,1]
	s_nop 0
	v_xor_b32_e32 v40, 0x80000000, v21
	v_mov_b32_e32 v41, v20
	v_pk_mul_f32 v[40:41], v[40:41], v[34:35] op_sel_hi:[1,0] neg_lo:[0,1] neg_hi:[0,1]
	s_nop 0
	v_pk_fma_f32 v[46:47], v[20:21], v[30:31], v[40:41] op_sel_hi:[1,0,1]
	v_pk_add_f32 v[20:21], v[22:23], v[48:49]
	v_pk_add_f32 v[22:23], v[22:23], v[48:49] neg_lo:[0,1] neg_hi:[0,1]
	s_nop 0
	v_xor_b32_e32 v40, 0x80000000, v23
	v_mov_b32_e32 v41, v22
	v_pk_mul_f32 v[40:41], v[40:41], v[36:37] op_sel_hi:[1,0] neg_lo:[0,1] neg_hi:[0,1]
	s_nop 0
	v_pk_fma_f32 v[50:51], v[22:23], v[32:33], v[40:41] op_sel_hi:[1,0,1]
	s_waitcnt lgkmcnt(5)
	v_pk_add_f32 v[22:23], v[24:25], v[52:53]
	v_pk_add_f32 v[24:25], v[24:25], v[52:53] neg_lo:[0,1] neg_hi:[0,1]
	s_nop 0
	v_xor_b32_e32 v40, 0x80000000, v25
	v_mov_b32_e32 v41, v24
	v_pk_mul_f32 v[40:41], v[40:41], v[10:11] op_sel_hi:[1,0] neg_lo:[0,1] neg_hi:[0,1]
	s_nop 0
	v_pk_fma_f32 v[52:53], v[24:25], v[10:11], v[40:41] op_sel_hi:[1,0,1]
	v_pk_add_f32 v[24:25], v[26:27], v[54:55]
	v_pk_add_f32 v[26:27], v[26:27], v[54:55] neg_lo:[0,1] neg_hi:[0,1]
	s_nop 0
	v_pk_mul_f32 v[40:41], v[26:27], v[36:37] op_sel_hi:[1,0]
	v_xor_b32_e32 v48, 0x80000000, v27
	v_mov_b32_e32 v49, v26
	v_pk_fma_f32 v[54:55], v[48:49], v[32:33], v[40:41] op_sel_hi:[1,0,1] neg_lo:[0,1,0] neg_hi:[0,1,0]
	s_waitcnt lgkmcnt(4)
	v_pk_add_f32 v[40:41], v[56:57], v[92:93] neg_lo:[0,1] neg_hi:[0,1]
	v_pk_add_f32 v[26:27], v[56:57], v[92:93]
	v_pk_mul_f32 v[48:49], v[40:41], v[34:35] op_sel_hi:[1,0]
	v_xor_b32_e32 v56, 0x80000000, v41
	v_mov_b32_e32 v57, v40
	v_pk_fma_f32 v[56:57], v[56:57], v[30:31], v[48:49] op_sel_hi:[1,0,1] neg_lo:[0,1,0] neg_hi:[0,1,0]
	v_pk_add_f32 v[48:49], v[58:59], v[94:95] neg_lo:[0,1] neg_hi:[0,1]
	v_pk_add_f32 v[40:41], v[58:59], v[94:95]
	v_pk_mul_f32 v[58:59], v[48:49], v[44:45] op_sel_hi:[1,0]
	v_xor_b32_e32 v92, 0x80000000, v49
	v_mov_b32_e32 v93, v48
	s_waitcnt lgkmcnt(3)
	v_pk_add_f32 v[48:49], v[76:77], v[96:97]
	v_pk_add_f32 v[76:77], v[76:77], v[96:97] neg_lo:[0,1] neg_hi:[0,1]
	v_pk_fma_f32 v[58:59], v[92:93], v[28:29], v[58:59] op_sel_hi:[1,0,1] neg_lo:[0,1,0] neg_hi:[0,1,0]
	v_xor_b32_e32 v93, 0x80000000, v76
	v_mov_b32_e32 v92, v77
	v_pk_add_f32 v[76:77], v[78:79], v[98:99]
	v_pk_add_f32 v[78:79], v[78:79], v[98:99] neg_lo:[0,1] neg_hi:[0,1]
	s_nop 0
	v_pk_mul_f32 v[94:95], v[78:79], v[44:45] op_sel_hi:[1,0] neg_lo:[0,1] neg_hi:[0,1]
	v_xor_b32_e32 v96, 0x80000000, v79
	v_mov_b32_e32 v97, v78
	v_pk_fma_f32 v[78:79], v[96:97], v[28:29], v[94:95] op_sel_hi:[1,0,1] neg_lo:[0,1,0] neg_hi:[0,1,0]
	s_waitcnt lgkmcnt(2)
	v_pk_add_f32 v[94:95], v[80:81], v[100:101]
	v_pk_add_f32 v[80:81], v[80:81], v[100:101] neg_lo:[0,1] neg_hi:[0,1]
	s_nop 0
	v_pk_mul_f32 v[96:97], v[80:81], v[34:35] op_sel_hi:[1,0] neg_lo:[0,1] neg_hi:[0,1]
	v_xor_b32_e32 v98, 0x80000000, v81
	v_mov_b32_e32 v99, v80
	v_pk_fma_f32 v[80:81], v[98:99], v[30:31], v[96:97] op_sel_hi:[1,0,1] neg_lo:[0,1,0] neg_hi:[0,1,0]
	v_pk_add_f32 v[96:97], v[82:83], v[102:103]
	v_pk_add_f32 v[82:83], v[82:83], v[102:103] neg_lo:[0,1] neg_hi:[0,1]
	s_nop 0
	v_pk_mul_f32 v[98:99], v[82:83], v[36:37] op_sel_hi:[1,0] neg_lo:[0,1] neg_hi:[0,1]
	v_xor_b32_e32 v100, 0x80000000, v83
	v_mov_b32_e32 v101, v82
	v_pk_fma_f32 v[82:83], v[100:101], v[32:33], v[98:99] op_sel_hi:[1,0,1] neg_lo:[0,1,0] neg_hi:[0,1,0]
	s_waitcnt lgkmcnt(1)
	v_pk_add_f32 v[98:99], v[84:85], v[104:105]
	v_pk_add_f32 v[84:85], v[84:85], v[104:105] neg_lo:[0,1] neg_hi:[0,1]
	s_nop 0
	v_xor_b32_e32 v100, 0x80000000, v85
	v_mov_b32_e32 v101, v84
	v_pk_mul_f32 v[100:101], v[100:101], v[10:11] op_sel_hi:[1,0] neg_lo:[0,1] neg_hi:[0,1]
	s_nop 0
	v_pk_fma_f32 v[84:85], v[84:85], v[10:11], v[100:101] op_sel_hi:[1,0,1] neg_lo:[0,1,0] neg_hi:[0,1,0]
	v_pk_add_f32 v[100:101], v[86:87], v[106:107]
	v_pk_add_f32 v[86:87], v[86:87], v[106:107] neg_lo:[0,1] neg_hi:[0,1]
	s_nop 0
	v_xor_b32_e32 v102, 0x80000000, v87
	v_mov_b32_e32 v103, v86
	v_pk_mul_f32 v[36:37], v[102:103], v[36:37] op_sel_hi:[1,0] neg_lo:[0,1] neg_hi:[0,1]
	s_nop 0
	v_pk_fma_f32 v[86:87], v[86:87], v[32:33], v[36:37] op_sel_hi:[1,0,1] neg_lo:[0,1,0] neg_hi:[0,1,0]
	s_waitcnt lgkmcnt(0)
	v_pk_add_f32 v[36:37], v[88:89], v[108:109] neg_lo:[0,1] neg_hi:[0,1]
	v_pk_add_f32 v[32:33], v[88:89], v[108:109]
	v_xor_b32_e32 v88, 0x80000000, v37
	v_mov_b32_e32 v89, v36
	v_pk_mul_f32 v[88:89], v[88:89], v[34:35] op_sel_hi:[1,0] neg_lo:[0,1] neg_hi:[0,1]
	s_nop 0
	v_pk_fma_f32 v[88:89], v[36:37], v[30:31], v[88:89] op_sel_hi:[1,0,1] neg_lo:[0,1,0] neg_hi:[0,1,0]
	v_pk_add_f32 v[36:37], v[90:91], v[110:111]
	v_pk_add_f32 v[90:91], v[90:91], v[110:111] neg_lo:[0,1] neg_hi:[0,1]
	s_nop 0
	v_xor_b32_e32 v102, 0x80000000, v91
	v_mov_b32_e32 v103, v90
	v_pk_mul_f32 v[44:45], v[102:103], v[44:45] op_sel_hi:[1,0] neg_lo:[0,1] neg_hi:[0,1]
	s_nop 0
	v_pk_fma_f32 v[90:91], v[90:91], v[28:29], v[44:45] op_sel_hi:[1,0,1] neg_lo:[0,1,0] neg_hi:[0,1,0]
	v_pk_add_f32 v[44:45], v[16:17], v[76:77]
	v_pk_add_f32 v[16:17], v[16:17], v[76:77] neg_lo:[0,1] neg_hi:[0,1]
	v_pk_add_f32 v[28:29], v[112:113], v[48:49]
	v_xor_b32_e32 v76, 0x80000000, v17
	v_mov_b32_e32 v77, v16
	v_pk_mul_f32 v[76:77], v[76:77], v[34:35] op_sel_hi:[1,0] neg_lo:[0,1] neg_hi:[0,1]
	v_pk_add_f32 v[48:49], v[112:113], v[48:49] neg_lo:[0,1] neg_hi:[0,1]
	v_pk_fma_f32 v[76:77], v[16:17], v[30:31], v[76:77] op_sel_hi:[1,0,1]
	v_pk_add_f32 v[16:17], v[18:19], v[94:95]
	v_pk_add_f32 v[18:19], v[18:19], v[94:95] neg_lo:[0,1] neg_hi:[0,1]
	s_nop 0
	v_xor_b32_e32 v94, 0x80000000, v19
	v_mov_b32_e32 v95, v18
	v_pk_mul_f32 v[94:95], v[94:95], v[10:11] op_sel_hi:[1,0] neg_lo:[0,1] neg_hi:[0,1]
	s_nop 0
	v_pk_fma_f32 v[18:19], v[18:19], v[10:11], v[94:95] op_sel_hi:[1,0,1]
	v_pk_add_f32 v[94:95], v[20:21], v[96:97]
	v_pk_add_f32 v[20:21], v[20:21], v[96:97] neg_lo:[0,1] neg_hi:[0,1]
	s_nop 0
	v_pk_mul_f32 v[96:97], v[20:21], v[34:35] op_sel_hi:[1,0]
	v_xor_b32_e32 v102, 0x80000000, v21
	v_mov_b32_e32 v103, v20
	v_pk_add_f32 v[20:21], v[22:23], v[98:99]
	v_pk_add_f32 v[22:23], v[22:23], v[98:99] neg_lo:[0,1] neg_hi:[0,1]
	v_pk_fma_f32 v[96:97], v[102:103], v[30:31], v[96:97] op_sel_hi:[1,0,1] neg_lo:[0,1,0] neg_hi:[0,1,0]
	v_xor_b32_e32 v99, 0x80000000, v22
	v_mov_b32_e32 v98, v23
	v_pk_add_f32 v[22:23], v[24:25], v[100:101]
	v_pk_add_f32 v[24:25], v[24:25], v[100:101] neg_lo:[0,1] neg_hi:[0,1]
	s_nop 0
	v_pk_mul_f32 v[100:101], v[24:25], v[34:35] op_sel_hi:[1,0] neg_lo:[0,1] neg_hi:[0,1]
	v_xor_b32_e32 v102, 0x80000000, v25
	v_mov_b32_e32 v103, v24
	v_pk_add_f32 v[24:25], v[26:27], v[32:33]
	v_pk_add_f32 v[26:27], v[26:27], v[32:33] neg_lo:[0,1] neg_hi:[0,1]
	v_pk_fma_f32 v[100:101], v[102:103], v[30:31], v[100:101] op_sel_hi:[1,0,1] neg_lo:[0,1,0] neg_hi:[0,1,0]
	v_xor_b32_e32 v32, 0x80000000, v27
	v_mov_b32_e32 v33, v26
	v_pk_mul_f32 v[32:33], v[32:33], v[10:11] op_sel_hi:[1,0] neg_lo:[0,1] neg_hi:[0,1]
	v_pk_add_f32 v[102:103], v[28:29], v[20:21] neg_lo:[0,1] neg_hi:[0,1]
	v_pk_fma_f32 v[26:27], v[26:27], v[10:11], v[32:33] op_sel_hi:[1,0,1] neg_lo:[0,1,0] neg_hi:[0,1,0]
	v_pk_add_f32 v[32:33], v[40:41], v[36:37]
	v_pk_add_f32 v[36:37], v[40:41], v[36:37] neg_lo:[0,1] neg_hi:[0,1]
	s_nop 0
	v_xor_b32_e32 v40, 0x80000000, v37
	v_mov_b32_e32 v41, v36
	v_pk_mul_f32 v[40:41], v[40:41], v[34:35] op_sel_hi:[1,0] neg_lo:[0,1] neg_hi:[0,1]
	s_nop 0
	v_pk_fma_f32 v[40:41], v[36:37], v[30:31], v[40:41] op_sel_hi:[1,0,1] neg_lo:[0,1,0] neg_hi:[0,1,0]
	v_pk_add_f32 v[36:37], v[28:29], v[20:21]
	v_pk_add_f32 v[20:21], v[44:45], v[22:23]
	v_pk_add_f32 v[22:23], v[44:45], v[22:23] neg_lo:[0,1] neg_hi:[0,1]
	s_nop 0
	v_xor_b32_e32 v28, 0x80000000, v23
	v_mov_b32_e32 v29, v22
	v_pk_mul_f32 v[28:29], v[28:29], v[10:11] op_sel_hi:[1,0] neg_lo:[0,1] neg_hi:[0,1]
	s_nop 0
	v_pk_fma_f32 v[22:23], v[22:23], v[10:11], v[28:29] op_sel_hi:[1,0,1]
	v_pk_add_f32 v[28:29], v[16:17], v[24:25]
	v_pk_add_f32 v[16:17], v[16:17], v[24:25] neg_lo:[0,1] neg_hi:[0,1]
	s_nop 0
	v_xor_b32_e32 v25, 0x80000000, v16
	v_mov_b32_e32 v24, v17
	v_pk_add_f32 v[16:17], v[94:95], v[32:33]
	v_pk_add_f32 v[32:33], v[94:95], v[32:33] neg_lo:[0,1] neg_hi:[0,1]
	s_nop 0
	v_xor_b32_e32 v44, 0x80000000, v33
	v_mov_b32_e32 v45, v32
	v_pk_mul_f32 v[44:45], v[44:45], v[10:11] op_sel_hi:[1,0] neg_lo:[0,1] neg_hi:[0,1]
	s_nop 0
	v_pk_fma_f32 v[32:33], v[32:33], v[10:11], v[44:45] op_sel_hi:[1,0,1] neg_lo:[0,1,0] neg_hi:[0,1,0]
	v_pk_add_f32 v[44:45], v[36:37], v[28:29]
	v_pk_add_f32 v[36:37], v[36:37], v[28:29] neg_lo:[0,1] neg_hi:[0,1]
	v_pk_add_f32 v[28:29], v[20:21], v[16:17]
	v_pk_add_f32 v[16:17], v[20:21], v[16:17] neg_lo:[0,1] neg_hi:[0,1]
	v_pk_add_f32 v[94:95], v[44:45], v[28:29]
	v_xor_b32_e32 v21, 0x80000000, v16
	v_mov_b32_e32 v20, v17
	v_pk_add_f32 v[16:17], v[102:103], v[24:25]
	v_pk_add_f32 v[102:103], v[102:103], v[24:25] neg_lo:[0,1] neg_hi:[0,1]
	v_pk_add_f32 v[24:25], v[22:23], v[32:33]
	v_pk_add_f32 v[22:23], v[22:23], v[32:33] neg_lo:[0,1] neg_hi:[0,1]
	v_pk_add_f32 v[28:29], v[44:45], v[28:29] neg_lo:[0,1] neg_hi:[0,1]
	v_xor_b32_e32 v33, 0x80000000, v22
	v_mov_b32_e32 v32, v23
	v_pk_add_f32 v[22:23], v[48:49], v[98:99]
	v_pk_add_f32 v[98:99], v[48:49], v[98:99] neg_lo:[0,1] neg_hi:[0,1]
	v_pk_add_f32 v[48:49], v[76:77], v[100:101] neg_lo:[0,1] neg_hi:[0,1]
	v_pk_add_f32 v[44:45], v[36:37], v[20:21]
	v_pk_add_f32 v[20:21], v[36:37], v[20:21] neg_lo:[0,1] neg_hi:[0,1]
	v_pk_add_f32 v[104:105], v[16:17], v[24:25]
	v_pk_add_f32 v[24:25], v[16:17], v[24:25] neg_lo:[0,1] neg_hi:[0,1]
	v_pk_add_f32 v[36:37], v[102:103], v[32:33]
	v_pk_add_f32 v[16:17], v[102:103], v[32:33] neg_lo:[0,1] neg_hi:[0,1]
	v_pk_add_f32 v[32:33], v[76:77], v[100:101]
	v_xor_b32_e32 v76, 0x80000000, v49
	v_mov_b32_e32 v77, v48
	v_pk_mul_f32 v[76:77], v[10:11], v[76:77] op_sel_hi:[0,1] neg_lo:[1,0] neg_hi:[1,0]
	v_pk_fma_f32 v[76:77], v[10:11], v[48:49], v[76:77] op_sel_hi:[0,1,1]
	v_pk_add_f32 v[48:49], v[18:19], v[26:27]
	v_pk_add_f32 v[18:19], v[18:19], v[26:27] neg_lo:[0,1] neg_hi:[0,1]
	s_nop 0
	v_xor_b32_e32 v27, 0x80000000, v18
	v_mov_b32_e32 v26, v19
	v_pk_add_f32 v[18:19], v[96:97], v[40:41]
	v_pk_add_f32 v[40:41], v[96:97], v[40:41] neg_lo:[0,1] neg_hi:[0,1]
	s_nop 0
	v_xor_b32_e32 v96, 0x80000000, v41
	v_mov_b32_e32 v97, v40
	v_pk_mul_f32 v[96:97], v[10:11], v[96:97] op_sel_hi:[0,1] neg_lo:[1,0] neg_hi:[1,0]
	v_pk_fma_f32 v[40:41], v[10:11], v[40:41], v[96:97] op_sel_hi:[0,1,1] neg_lo:[1,0,0] neg_hi:[1,0,0]
	v_pk_add_f32 v[96:97], v[22:23], v[48:49]
	v_pk_add_f32 v[22:23], v[22:23], v[48:49] neg_lo:[0,1] neg_hi:[0,1]
	v_pk_add_f32 v[48:49], v[32:33], v[18:19]
	v_pk_add_f32 v[18:19], v[32:33], v[18:19] neg_lo:[0,1] neg_hi:[0,1]
	v_pk_add_f32 v[102:103], v[96:97], v[48:49]
	v_xor_b32_e32 v101, 0x80000000, v18
	v_mov_b32_e32 v100, v19
	v_pk_add_f32 v[32:33], v[96:97], v[48:49] neg_lo:[0,1] neg_hi:[0,1]
	v_pk_add_f32 v[18:19], v[98:99], v[26:27]
	v_pk_add_f32 v[96:97], v[98:99], v[26:27] neg_lo:[0,1] neg_hi:[0,1]
	v_pk_add_f32 v[26:27], v[76:77], v[40:41]
	v_pk_add_f32 v[40:41], v[76:77], v[40:41] neg_lo:[0,1] neg_hi:[0,1]
	v_pk_add_f32 v[98:99], v[18:19], v[26:27]
	v_xor_b32_e32 v77, 0x80000000, v40
	v_mov_b32_e32 v76, v41
	v_pk_add_f32 v[26:27], v[18:19], v[26:27] neg_lo:[0,1] neg_hi:[0,1]
	v_pk_add_f32 v[40:41], v[96:97], v[76:77]
	v_pk_add_f32 v[18:19], v[96:97], v[76:77] neg_lo:[0,1] neg_hi:[0,1]
	v_pk_add_f32 v[76:77], v[38:39], v[92:93]
	v_pk_add_f32 v[92:93], v[38:39], v[92:93] neg_lo:[0,1] neg_hi:[0,1]
	v_pk_add_f32 v[38:39], v[42:43], v[78:79]
	v_pk_add_f32 v[42:43], v[42:43], v[78:79] neg_lo:[0,1] neg_hi:[0,1]
	v_pk_add_f32 v[48:49], v[22:23], v[100:101]
	v_xor_b32_e32 v78, 0x80000000, v43
	v_mov_b32_e32 v79, v42
	v_pk_mul_f32 v[78:79], v[34:35], v[78:79] op_sel_hi:[0,1] neg_lo:[1,0] neg_hi:[1,0]
	v_pk_fma_f32 v[42:43], v[30:31], v[42:43], v[78:79] op_sel_hi:[0,1,1]
	v_pk_add_f32 v[78:79], v[46:47], v[80:81]
	v_pk_add_f32 v[46:47], v[46:47], v[80:81] neg_lo:[0,1] neg_hi:[0,1]
	v_pk_add_f32 v[22:23], v[22:23], v[100:101] neg_lo:[0,1] neg_hi:[0,1]
	v_xor_b32_e32 v80, 0x80000000, v47
	v_mov_b32_e32 v81, v46
	v_pk_mul_f32 v[80:81], v[10:11], v[80:81] op_sel_hi:[0,1] neg_lo:[1,0] neg_hi:[1,0]
	v_pk_fma_f32 v[80:81], v[10:11], v[46:47], v[80:81] op_sel_hi:[0,1,1]
	v_pk_add_f32 v[46:47], v[50:51], v[82:83]
	v_pk_add_f32 v[50:51], v[50:51], v[82:83] neg_lo:[0,1] neg_hi:[0,1]
	s_nop 0
	v_xor_b32_e32 v82, 0x80000000, v51
	v_mov_b32_e32 v83, v50
	v_pk_mul_f32 v[82:83], v[30:31], v[82:83] op_sel_hi:[0,1] neg_lo:[1,0] neg_hi:[1,0]
	v_pk_fma_f32 v[50:51], v[34:35], v[50:51], v[82:83] op_sel_hi:[0,1,1]
	v_pk_add_f32 v[82:83], v[52:53], v[84:85]
	v_pk_add_f32 v[52:53], v[52:53], v[84:85] neg_lo:[0,1] neg_hi:[0,1]
	s_nop 0
	v_xor_b32_e32 v85, 0x80000000, v52
	v_mov_b32_e32 v84, v53
	v_pk_add_f32 v[52:53], v[54:55], v[86:87]
	v_pk_add_f32 v[54:55], v[54:55], v[86:87] neg_lo:[0,1] neg_hi:[0,1]
	s_nop 0
	v_xor_b32_e32 v86, 0x80000000, v55
	v_mov_b32_e32 v87, v54
	v_pk_mul_f32 v[86:87], v[30:31], v[86:87] op_sel_hi:[0,1] neg_lo:[1,0] neg_hi:[1,0]
	v_pk_fma_f32 v[54:55], v[34:35], v[54:55], v[86:87] op_sel_hi:[0,1,1] neg_lo:[1,0,0] neg_hi:[1,0,0]
	v_pk_add_f32 v[86:87], v[56:57], v[88:89]
	v_pk_add_f32 v[56:57], v[56:57], v[88:89] neg_lo:[0,1] neg_hi:[0,1]
	s_nop 0
	v_xor_b32_e32 v88, 0x80000000, v57
	v_mov_b32_e32 v89, v56
	v_pk_mul_f32 v[88:89], v[10:11], v[88:89] op_sel_hi:[0,1] neg_lo:[1,0] neg_hi:[1,0]
	v_pk_fma_f32 v[56:57], v[10:11], v[56:57], v[88:89] op_sel_hi:[0,1,1] neg_lo:[1,0,0] neg_hi:[1,0,0]
	v_pk_add_f32 v[88:89], v[58:59], v[90:91]
	v_pk_add_f32 v[58:59], v[58:59], v[90:91] neg_lo:[0,1] neg_hi:[0,1]
	s_nop 0
	v_xor_b32_e32 v90, 0x80000000, v59
	v_mov_b32_e32 v91, v58
	v_pk_mul_f32 v[34:35], v[34:35], v[90:91] op_sel_hi:[0,1] neg_lo:[1,0] neg_hi:[1,0]
	v_pk_fma_f32 v[34:35], v[30:31], v[58:59], v[34:35] op_sel_hi:[0,1,1] neg_lo:[1,0,0] neg_hi:[1,0,0]
	v_pk_add_f32 v[30:31], v[76:77], v[82:83]
	v_pk_add_f32 v[58:59], v[76:77], v[82:83] neg_lo:[0,1] neg_hi:[0,1]
	v_pk_add_f32 v[76:77], v[52:53], v[38:39]
	v_pk_add_f32 v[38:39], v[38:39], v[52:53] neg_lo:[0,1] neg_hi:[0,1]
	s_nop 0
	v_xor_b32_e32 v52, 0x80000000, v39
	v_mov_b32_e32 v53, v38
	v_pk_mul_f32 v[52:53], v[10:11], v[52:53] op_sel_hi:[0,1] neg_lo:[1,0] neg_hi:[1,0]
	v_pk_fma_f32 v[52:53], v[10:11], v[38:39], v[52:53] op_sel_hi:[0,1,1]
	v_pk_add_f32 v[38:39], v[78:79], v[86:87]
	v_pk_add_f32 v[78:79], v[78:79], v[86:87] neg_lo:[0,1] neg_hi:[0,1]
	s_nop 0
	v_xor_b32_e32 v83, 0x80000000, v78
	v_mov_b32_e32 v82, v79
	v_pk_add_f32 v[78:79], v[46:47], v[88:89]
	v_pk_add_f32 v[46:47], v[46:47], v[88:89] neg_lo:[0,1] neg_hi:[0,1]
	v_pk_add_f32 v[88:89], v[76:77], v[78:79]
	v_xor_b32_e32 v86, 0x80000000, v47
	v_mov_b32_e32 v87, v46
	v_pk_mul_f32 v[86:87], v[10:11], v[86:87] op_sel_hi:[0,1] neg_lo:[1,0] neg_hi:[1,0]
	v_pk_fma_f32 v[46:47], v[10:11], v[46:47], v[86:87] op_sel_hi:[0,1,1] neg_lo:[1,0,0] neg_hi:[1,0,0]
	v_pk_add_f32 v[86:87], v[30:31], v[38:39]
	v_pk_add_f32 v[30:31], v[30:31], v[38:39] neg_lo:[0,1] neg_hi:[0,1]
	v_pk_add_f32 v[38:39], v[76:77], v[78:79] neg_lo:[0,1] neg_hi:[0,1]
	v_pk_add_f32 v[78:79], v[86:87], v[88:89] neg_lo:[0,1] neg_hi:[0,1]
	v_xor_b32_e32 v77, 0x80000000, v38
	v_mov_b32_e32 v76, v39
	v_pk_add_f32 v[90:91], v[30:31], v[76:77]
	v_pk_add_f32 v[38:39], v[30:31], v[76:77] neg_lo:[0,1] neg_hi:[0,1]
	v_pk_add_f32 v[76:77], v[52:53], v[46:47]
	v_pk_add_f32 v[46:47], v[52:53], v[46:47] neg_lo:[0,1] neg_hi:[0,1]
	v_pk_add_f32 v[30:31], v[58:59], v[82:83]
	v_pk_add_f32 v[58:59], v[58:59], v[82:83] neg_lo:[0,1] neg_hi:[0,1]
	v_xor_b32_e32 v53, 0x80000000, v46
	v_mov_b32_e32 v52, v47
	v_pk_add_f32 v[82:83], v[30:31], v[76:77]
	v_pk_add_f32 v[46:47], v[30:31], v[76:77] neg_lo:[0,1] neg_hi:[0,1]
	v_pk_add_f32 v[76:77], v[58:59], v[52:53]
	v_pk_add_f32 v[30:31], v[58:59], v[52:53] neg_lo:[0,1] neg_hi:[0,1]
	v_pk_add_f32 v[52:53], v[92:93], v[84:85]
	v_pk_add_f32 v[58:59], v[92:93], v[84:85] neg_lo:[0,1] neg_hi:[0,1]
	v_pk_add_f32 v[84:85], v[54:55], v[42:43]
	v_pk_add_f32 v[42:43], v[42:43], v[54:55] neg_lo:[0,1] neg_hi:[0,1]
	v_pk_add_f32 v[86:87], v[86:87], v[88:89]
	v_xor_b32_e32 v54, 0x80000000, v43
	v_mov_b32_e32 v55, v42
	v_pk_mul_f32 v[54:55], v[10:11], v[54:55] op_sel_hi:[0,1] neg_lo:[1,0] neg_hi:[1,0]
	v_pk_fma_f32 v[54:55], v[10:11], v[42:43], v[54:55] op_sel_hi:[0,1,1]
	v_pk_add_f32 v[42:43], v[80:81], v[56:57]
	v_pk_add_f32 v[56:57], v[80:81], v[56:57] neg_lo:[0,1] neg_hi:[0,1]
	v_xor_b32_e32 v88, 0x80000000, v87
	v_xor_b32_e32 v81, 0x80000000, v56
	v_mov_b32_e32 v80, v57
	v_pk_add_f32 v[56:57], v[50:51], v[34:35]
	v_pk_add_f32 v[34:35], v[50:51], v[34:35] neg_lo:[0,1] neg_hi:[0,1]
	v_mov_b32_e32 v89, v87
	v_xor_b32_e32 v50, 0x80000000, v35
	v_mov_b32_e32 v51, v34
	v_pk_mul_f32 v[50:51], v[10:11], v[50:51] op_sel_hi:[0,1] neg_lo:[1,0] neg_hi:[1,0]
	v_pk_fma_f32 v[34:35], v[10:11], v[34:35], v[50:51] op_sel_hi:[0,1,1] neg_lo:[1,0,0] neg_hi:[1,0,0]
	v_pk_add_f32 v[50:51], v[52:53], v[42:43]
	v_pk_add_f32 v[42:43], v[52:53], v[42:43] neg_lo:[0,1] neg_hi:[0,1]
	v_pk_add_f32 v[52:53], v[84:85], v[56:57]
	v_pk_add_f32 v[56:57], v[84:85], v[56:57] neg_lo:[0,1] neg_hi:[0,1]
	s_nop 0
	v_xor_b32_e32 v85, 0x80000000, v56
	v_mov_b32_e32 v84, v57
	v_pk_add_f32 v[56:57], v[50:51], v[52:53]
	v_pk_add_f32 v[50:51], v[50:51], v[52:53] neg_lo:[0,1] neg_hi:[0,1]
	v_pk_add_f32 v[52:53], v[42:43], v[84:85]
	v_pk_add_f32 v[42:43], v[42:43], v[84:85] neg_lo:[0,1] neg_hi:[0,1]
	v_pk_add_f32 v[84:85], v[58:59], v[80:81]
	v_pk_add_f32 v[58:59], v[58:59], v[80:81] neg_lo:[0,1] neg_hi:[0,1]
	v_pk_add_f32 v[80:81], v[54:55], v[34:35]
	v_pk_add_f32 v[34:35], v[54:55], v[34:35] neg_lo:[0,1] neg_hi:[0,1]
	v_pk_add_f32 v[92:93], v[84:85], v[80:81]
	v_xor_b32_e32 v55, 0x80000000, v34
	v_mov_b32_e32 v54, v35
	v_pk_add_f32 v[80:81], v[84:85], v[80:81] neg_lo:[0,1] neg_hi:[0,1]
	v_pk_add_f32 v[84:85], v[58:59], v[54:55]
	v_pk_add_f32 v[34:35], v[58:59], v[54:55] neg_lo:[0,1] neg_hi:[0,1]
	v_xor_b32_e32 v54, 0x80000000, v95
	v_mov_b32_e32 v55, v95
	v_pk_fma_f32 v[58:59], v[14:15], s[92:93], v[14:15] op_sel:[1,0,0] op_sel_hi:[0,1,1]
	v_pk_mul_f32 v[54:55], v[54:55], s[14:15]
	v_pk_mul_f32 v[88:89], v[58:59], v[88:89] op_sel:[1,0] op_sel_hi:[0,1]
	v_pk_fma_f32 v[54:55], v[94:95], s[42:43], v[54:55] op_sel_hi:[0,1,1]
	v_pk_fma_f32 v[86:87], v[58:59], v[86:87], v[88:89] op_sel_hi:[1,0,1]
	ds_write2_b64 v74, v[54:55], v[86:87] offset1:16
	v_xor_b32_e32 v54, 0x80000000, v59
	v_mov_b32_e32 v55, v59
	v_pk_mul_f32 v[54:55], v[14:15], v[54:55] op_sel:[1,0] op_sel_hi:[0,1]
	v_pk_fma_f32 v[54:55], v[14:15], v[58:59], v[54:55] op_sel_hi:[1,0,1]
	v_xor_b32_e32 v58, 0x80000000, v103
	v_mov_b32_e32 v59, v103
	v_xor_b32_e32 v74, 0x80000000, v55
	v_mov_b32_e32 v75, v55
	v_pk_mul_f32 v[58:59], v[54:55], v[58:59] op_sel:[1,0] op_sel_hi:[0,1]
	v_pk_mul_f32 v[74:75], v[14:15], v[74:75] op_sel:[1,0] op_sel_hi:[0,1]
	v_pk_fma_f32 v[58:59], v[54:55], v[102:103], v[58:59] op_sel_hi:[1,0,1]
	v_pk_fma_f32 v[54:55], v[14:15], v[54:55], v[74:75] op_sel_hi:[1,0,1]
	v_xor_b32_e32 v74, 0x80000000, v57
	v_mov_b32_e32 v75, v57
	v_pk_mul_f32 v[74:75], v[54:55], v[74:75] op_sel:[1,0] op_sel_hi:[0,1]
	v_pk_fma_f32 v[56:57], v[54:55], v[56:57], v[74:75] op_sel_hi:[1,0,1]
	ds_write2_b64 v73, v[58:59], v[56:57] offset0:32 offset1:48
	v_xor_b32_e32 v56, 0x80000000, v55
	v_mov_b32_e32 v57, v55
	v_pk_mul_f32 v[56:57], v[14:15], v[56:57] op_sel:[1,0] op_sel_hi:[0,1]
	v_pk_fma_f32 v[54:55], v[14:15], v[54:55], v[56:57] op_sel_hi:[1,0,1]
	v_xor_b32_e32 v56, 0x80000000, v105
	v_mov_b32_e32 v57, v105
	v_xor_b32_e32 v58, 0x80000000, v55
	v_mov_b32_e32 v59, v55
	v_pk_mul_f32 v[56:57], v[54:55], v[56:57] op_sel:[1,0] op_sel_hi:[0,1]
	v_pk_mul_f32 v[58:59], v[14:15], v[58:59] op_sel:[1,0] op_sel_hi:[0,1]
	v_pk_fma_f32 v[56:57], v[54:55], v[104:105], v[56:57] op_sel_hi:[1,0,1]
	v_pk_fma_f32 v[54:55], v[14:15], v[54:55], v[58:59] op_sel_hi:[1,0,1]
	v_xor_b32_e32 v58, 0x80000000, v83
	v_mov_b32_e32 v59, v83
	v_pk_mul_f32 v[58:59], v[54:55], v[58:59] op_sel:[1,0] op_sel_hi:[0,1]
	v_pk_fma_f32 v[58:59], v[54:55], v[82:83], v[58:59] op_sel_hi:[1,0,1]
	ds_write2_b64 v72, v[56:57], v[58:59] offset0:64 offset1:80
	v_xor_b32_e32 v56, 0x80000000, v55
	v_mov_b32_e32 v57, v55
	v_pk_mul_f32 v[56:57], v[14:15], v[56:57] op_sel:[1,0] op_sel_hi:[0,1]
	v_pk_fma_f32 v[54:55], v[14:15], v[54:55], v[56:57] op_sel_hi:[1,0,1]
	v_xor_b32_e32 v56, 0x80000000, v99
	v_mov_b32_e32 v57, v99
	v_xor_b32_e32 v58, 0x80000000, v55
	v_mov_b32_e32 v59, v55
	v_pk_mul_f32 v[56:57], v[54:55], v[56:57] op_sel:[1,0] op_sel_hi:[0,1]
	v_pk_mul_f32 v[58:59], v[14:15], v[58:59] op_sel:[1,0] op_sel_hi:[0,1]
	v_pk_fma_f32 v[56:57], v[54:55], v[98:99], v[56:57] op_sel_hi:[1,0,1]
	v_pk_fma_f32 v[54:55], v[14:15], v[54:55], v[58:59] op_sel_hi:[1,0,1]
	v_xor_b32_e32 v58, 0x80000000, v93
	v_mov_b32_e32 v59, v93
	v_pk_mul_f32 v[58:59], v[54:55], v[58:59] op_sel:[1,0] op_sel_hi:[0,1]
	v_pk_fma_f32 v[58:59], v[54:55], v[92:93], v[58:59] op_sel_hi:[1,0,1]
	ds_write2_b64 v71, v[56:57], v[58:59] offset0:96 offset1:112
	v_xor_b32_e32 v56, 0x80000000, v55
	v_mov_b32_e32 v57, v55
	v_pk_mul_f32 v[56:57], v[14:15], v[56:57] op_sel:[1,0] op_sel_hi:[0,1]
	v_pk_fma_f32 v[54:55], v[14:15], v[54:55], v[56:57] op_sel_hi:[1,0,1]
	v_xor_b32_e32 v56, 0x80000000, v45
	v_mov_b32_e32 v57, v45
	v_pk_mul_f32 v[56:57], v[54:55], v[56:57] op_sel:[1,0] op_sel_hi:[0,1]
	v_pk_fma_f32 v[44:45], v[54:55], v[44:45], v[56:57] op_sel_hi:[1,0,1]
	v_xor_b32_e32 v56, 0x80000000, v55
	v_mov_b32_e32 v57, v55
	v_pk_mul_f32 v[56:57], v[14:15], v[56:57] op_sel:[1,0] op_sel_hi:[0,1]
	v_pk_fma_f32 v[54:55], v[14:15], v[54:55], v[56:57] op_sel_hi:[1,0,1]
	v_xor_b32_e32 v56, 0x80000000, v91
	v_mov_b32_e32 v57, v91
	v_pk_mul_f32 v[56:57], v[54:55], v[56:57] op_sel:[1,0] op_sel_hi:[0,1]
	v_pk_fma_f32 v[56:57], v[54:55], v[90:91], v[56:57] op_sel_hi:[1,0,1]
	ds_write2_b64 v70, v[44:45], v[56:57] offset0:128 offset1:144
	v_xor_b32_e32 v44, 0x80000000, v55
	v_mov_b32_e32 v45, v55
	v_pk_mul_f32 v[44:45], v[14:15], v[44:45] op_sel:[1,0] op_sel_hi:[0,1]
	v_pk_fma_f32 v[44:45], v[14:15], v[54:55], v[44:45] op_sel_hi:[1,0,1]
	v_xor_b32_e32 v54, 0x80000000, v49
	v_mov_b32_e32 v55, v49
	v_pk_mul_f32 v[54:55], v[44:45], v[54:55] op_sel:[1,0] op_sel_hi:[0,1]
	v_pk_fma_f32 v[48:49], v[44:45], v[48:49], v[54:55] op_sel_hi:[1,0,1]
	v_xor_b32_e32 v54, 0x80000000, v45
	v_mov_b32_e32 v55, v45
	v_pk_mul_f32 v[54:55], v[14:15], v[54:55] op_sel:[1,0] op_sel_hi:[0,1]
	v_pk_fma_f32 v[44:45], v[14:15], v[44:45], v[54:55] op_sel_hi:[1,0,1]
	v_xor_b32_e32 v54, 0x80000000, v53
	v_mov_b32_e32 v55, v53
	v_pk_mul_f32 v[54:55], v[44:45], v[54:55] op_sel:[1,0] op_sel_hi:[0,1]
	v_pk_fma_f32 v[52:53], v[44:45], v[52:53], v[54:55] op_sel_hi:[1,0,1]
	ds_write2_b64 v69, v[48:49], v[52:53] offset0:160 offset1:176
	v_xor_b32_e32 v48, 0x80000000, v45
	v_mov_b32_e32 v49, v45
	v_pk_mul_f32 v[48:49], v[14:15], v[48:49] op_sel:[1,0] op_sel_hi:[0,1]
	v_pk_fma_f32 v[44:45], v[14:15], v[44:45], v[48:49] op_sel_hi:[1,0,1]
	v_xor_b32_e32 v48, 0x80000000, v37
	v_mov_b32_e32 v49, v37
	v_pk_mul_f32 v[48:49], v[48:49], v[44:45] op_sel:[0,1] op_sel_hi:[1,0]
	s_nop 0
	v_pk_fma_f32 v[36:37], v[36:37], v[44:45], v[48:49] op_sel_hi:[0,1,1]
	v_xor_b32_e32 v48, 0x80000000, v45
	v_mov_b32_e32 v49, v45
	v_pk_mul_f32 v[48:49], v[14:15], v[48:49] op_sel:[1,0] op_sel_hi:[0,1]
	v_pk_fma_f32 v[44:45], v[14:15], v[44:45], v[48:49] op_sel_hi:[1,0,1]
	v_xor_b32_e32 v48, 0x80000000, v77
	v_mov_b32_e32 v49, v77
	v_pk_mul_f32 v[48:49], v[44:45], v[48:49] op_sel:[1,0] op_sel_hi:[0,1]
	v_pk_fma_f32 v[48:49], v[44:45], v[76:77], v[48:49] op_sel_hi:[1,0,1]
	ds_write2_b64 v68, v[36:37], v[48:49] offset0:192 offset1:208
	v_xor_b32_e32 v36, 0x80000000, v45
	v_mov_b32_e32 v37, v45
	v_pk_mul_f32 v[36:37], v[14:15], v[36:37] op_sel:[1,0] op_sel_hi:[0,1]
	v_pk_fma_f32 v[36:37], v[14:15], v[44:45], v[36:37] op_sel_hi:[1,0,1]
	v_xor_b32_e32 v44, 0x80000000, v41
	v_mov_b32_e32 v45, v41
	v_pk_mul_f32 v[44:45], v[44:45], v[36:37] op_sel:[0,1] op_sel_hi:[1,0]
	s_nop 0
	v_pk_fma_f32 v[40:41], v[40:41], v[36:37], v[44:45] op_sel_hi:[0,1,1]
	v_xor_b32_e32 v44, 0x80000000, v37
	v_mov_b32_e32 v45, v37
	v_pk_mul_f32 v[44:45], v[14:15], v[44:45] op_sel:[1,0] op_sel_hi:[0,1]
	v_pk_fma_f32 v[36:37], v[14:15], v[36:37], v[44:45] op_sel_hi:[1,0,1]
	v_xor_b32_e32 v44, 0x80000000, v85
	v_mov_b32_e32 v45, v85
	v_pk_mul_f32 v[44:45], v[36:37], v[44:45] op_sel:[1,0] op_sel_hi:[0,1]
	v_pk_fma_f32 v[44:45], v[36:37], v[84:85], v[44:45] op_sel_hi:[1,0,1]
	ds_write2_b64 v67, v[40:41], v[44:45] offset0:224 offset1:240
	v_xor_b32_e32 v40, 0x80000000, v37
	v_mov_b32_e32 v41, v37
	v_pk_mul_f32 v[40:41], v[14:15], v[40:41] op_sel:[1,0] op_sel_hi:[0,1]
	v_pk_fma_f32 v[36:37], v[14:15], v[36:37], v[40:41] op_sel_hi:[1,0,1]
	v_xor_b32_e32 v40, 0x80000000, v29
	v_mov_b32_e32 v41, v29
	v_pk_mul_f32 v[40:41], v[40:41], v[36:37] op_sel:[0,1] op_sel_hi:[1,0]
	s_nop 0
	v_pk_fma_f32 v[28:29], v[28:29], v[36:37], v[40:41] op_sel_hi:[0,1,1]
	v_xor_b32_e32 v40, 0x80000000, v37
	v_mov_b32_e32 v41, v37
	v_pk_mul_f32 v[40:41], v[14:15], v[40:41] op_sel:[1,0] op_sel_hi:[0,1]
	v_pk_fma_f32 v[36:37], v[14:15], v[36:37], v[40:41] op_sel_hi:[1,0,1]
	v_xor_b32_e32 v40, 0x80000000, v79
	v_mov_b32_e32 v41, v79
	v_pk_mul_f32 v[40:41], v[40:41], v[36:37] op_sel:[0,1] op_sel_hi:[1,0]
	s_nop 0
	v_pk_fma_f32 v[40:41], v[78:79], v[36:37], v[40:41] op_sel_hi:[0,1,1]
	ds_write2_b64 v66, v[28:29], v[40:41] offset1:16
	v_xor_b32_e32 v28, 0x80000000, v37
	v_mov_b32_e32 v29, v37
	v_pk_mul_f32 v[28:29], v[14:15], v[28:29] op_sel:[1,0] op_sel_hi:[0,1]
	v_pk_fma_f32 v[28:29], v[14:15], v[36:37], v[28:29] op_sel_hi:[1,0,1]
	v_xor_b32_e32 v36, 0x80000000, v33
	v_mov_b32_e32 v37, v33
	v_pk_mul_f32 v[36:37], v[36:37], v[28:29] op_sel:[0,1] op_sel_hi:[1,0]
	s_nop 0
	v_pk_fma_f32 v[32:33], v[32:33], v[28:29], v[36:37] op_sel_hi:[0,1,1]
	v_xor_b32_e32 v36, 0x80000000, v29
	v_mov_b32_e32 v37, v29
	v_pk_mul_f32 v[36:37], v[14:15], v[36:37] op_sel:[1,0] op_sel_hi:[0,1]
	v_pk_fma_f32 v[28:29], v[14:15], v[28:29], v[36:37] op_sel_hi:[1,0,1]
	v_xor_b32_e32 v36, 0x80000000, v51
	v_mov_b32_e32 v37, v51
	v_pk_mul_f32 v[36:37], v[36:37], v[28:29] op_sel:[0,1] op_sel_hi:[1,0]
	s_nop 0
	v_pk_fma_f32 v[36:37], v[50:51], v[28:29], v[36:37] op_sel_hi:[0,1,1]
	ds_write2_b64 v65, v[32:33], v[36:37] offset0:32 offset1:48
	v_xor_b32_e32 v32, 0x80000000, v29
	v_mov_b32_e32 v33, v29
	v_pk_mul_f32 v[32:33], v[14:15], v[32:33] op_sel:[1,0] op_sel_hi:[0,1]
	v_pk_fma_f32 v[28:29], v[14:15], v[28:29], v[32:33] op_sel_hi:[1,0,1]
	v_xor_b32_e32 v32, 0x80000000, v25
	v_mov_b32_e32 v33, v25
	v_pk_mul_f32 v[32:33], v[32:33], v[28:29] op_sel:[0,1] op_sel_hi:[1,0]
	s_nop 0
	v_pk_fma_f32 v[24:25], v[24:25], v[28:29], v[32:33] op_sel_hi:[0,1,1]
	v_xor_b32_e32 v32, 0x80000000, v29
	v_mov_b32_e32 v33, v29
	v_pk_mul_f32 v[32:33], v[14:15], v[32:33] op_sel:[1,0] op_sel_hi:[0,1]
	v_pk_fma_f32 v[28:29], v[14:15], v[28:29], v[32:33] op_sel_hi:[1,0,1]
	v_xor_b32_e32 v32, 0x80000000, v47
	v_mov_b32_e32 v33, v47
	v_pk_mul_f32 v[32:33], v[32:33], v[28:29] op_sel:[0,1] op_sel_hi:[1,0]
	s_nop 0
	v_pk_fma_f32 v[32:33], v[46:47], v[28:29], v[32:33] op_sel_hi:[0,1,1]
	ds_write2_b64 v64, v[24:25], v[32:33] offset0:64 offset1:80
	v_xor_b32_e32 v24, 0x80000000, v29
	v_mov_b32_e32 v25, v29
	v_pk_mul_f32 v[24:25], v[14:15], v[24:25] op_sel:[1,0] op_sel_hi:[0,1]
	v_pk_fma_f32 v[24:25], v[14:15], v[28:29], v[24:25] op_sel_hi:[1,0,1]
	v_xor_b32_e32 v28, 0x80000000, v27
	v_mov_b32_e32 v29, v27
	v_pk_mul_f32 v[28:29], v[28:29], v[24:25] op_sel:[0,1] op_sel_hi:[1,0]
	s_nop 0
	v_pk_fma_f32 v[26:27], v[26:27], v[24:25], v[28:29] op_sel_hi:[0,1,1]
	v_xor_b32_e32 v28, 0x80000000, v25
	v_mov_b32_e32 v29, v25
	v_pk_mul_f32 v[28:29], v[14:15], v[28:29] op_sel:[1,0] op_sel_hi:[0,1]
	v_pk_fma_f32 v[24:25], v[14:15], v[24:25], v[28:29] op_sel_hi:[1,0,1]
	v_xor_b32_e32 v28, 0x80000000, v81
	v_mov_b32_e32 v29, v81
	v_pk_mul_f32 v[28:29], v[28:29], v[24:25] op_sel:[0,1] op_sel_hi:[1,0]
	s_nop 0
	v_pk_fma_f32 v[28:29], v[80:81], v[24:25], v[28:29] op_sel_hi:[0,1,1]
	ds_write2_b64 v63, v[26:27], v[28:29] offset0:96 offset1:112
	v_xor_b32_e32 v26, 0x80000000, v25
	v_mov_b32_e32 v27, v25
	v_pk_mul_f32 v[26:27], v[14:15], v[26:27] op_sel:[1,0] op_sel_hi:[0,1]
	v_pk_fma_f32 v[24:25], v[14:15], v[24:25], v[26:27] op_sel_hi:[1,0,1]
	v_xor_b32_e32 v26, 0x80000000, v21
	v_mov_b32_e32 v27, v21
	v_pk_mul_f32 v[26:27], v[26:27], v[24:25] op_sel:[0,1] op_sel_hi:[1,0]
	s_nop 0
	v_pk_fma_f32 v[20:21], v[20:21], v[24:25], v[26:27] op_sel_hi:[0,1,1]
	v_xor_b32_e32 v26, 0x80000000, v25
	v_mov_b32_e32 v27, v25
	v_pk_mul_f32 v[26:27], v[14:15], v[26:27] op_sel:[1,0] op_sel_hi:[0,1]
	v_pk_fma_f32 v[24:25], v[14:15], v[24:25], v[26:27] op_sel_hi:[1,0,1]
	v_xor_b32_e32 v26, 0x80000000, v39
	v_mov_b32_e32 v27, v39
	v_pk_mul_f32 v[26:27], v[26:27], v[24:25] op_sel:[0,1] op_sel_hi:[1,0]
	s_nop 0
	v_pk_fma_f32 v[26:27], v[38:39], v[24:25], v[26:27] op_sel_hi:[0,1,1]
	ds_write2_b64 v62, v[20:21], v[26:27] offset0:128 offset1:144
	v_xor_b32_e32 v20, 0x80000000, v25
	v_mov_b32_e32 v21, v25
	v_pk_mul_f32 v[20:21], v[14:15], v[20:21] op_sel:[1,0] op_sel_hi:[0,1]
	v_pk_fma_f32 v[20:21], v[14:15], v[24:25], v[20:21] op_sel_hi:[1,0,1]
	v_xor_b32_e32 v24, 0x80000000, v23
	v_mov_b32_e32 v25, v23
	v_pk_mul_f32 v[24:25], v[24:25], v[20:21] op_sel:[0,1] op_sel_hi:[1,0]
	s_nop 0
	v_pk_fma_f32 v[22:23], v[22:23], v[20:21], v[24:25] op_sel_hi:[0,1,1]
	v_xor_b32_e32 v24, 0x80000000, v21
	v_mov_b32_e32 v25, v21
	v_pk_mul_f32 v[24:25], v[14:15], v[24:25] op_sel:[1,0] op_sel_hi:[0,1]
	v_pk_fma_f32 v[20:21], v[14:15], v[20:21], v[24:25] op_sel_hi:[1,0,1]
	v_xor_b32_e32 v24, 0x80000000, v43
	v_mov_b32_e32 v25, v43
	v_pk_mul_f32 v[24:25], v[24:25], v[20:21] op_sel:[0,1] op_sel_hi:[1,0]
	s_nop 0
	v_pk_fma_f32 v[24:25], v[42:43], v[20:21], v[24:25] op_sel_hi:[0,1,1]
	ds_write2_b64 v61, v[22:23], v[24:25] offset0:160 offset1:176
	v_xor_b32_e32 v22, 0x80000000, v21
	v_mov_b32_e32 v23, v21
	v_pk_mul_f32 v[22:23], v[14:15], v[22:23] op_sel:[1,0] op_sel_hi:[0,1]
	v_pk_fma_f32 v[20:21], v[14:15], v[20:21], v[22:23] op_sel_hi:[1,0,1]
	v_xor_b32_e32 v22, 0x80000000, v17
	v_mov_b32_e32 v23, v17
	v_pk_mul_f32 v[22:23], v[22:23], v[20:21] op_sel:[0,1] op_sel_hi:[1,0]
	s_nop 0
	v_pk_fma_f32 v[16:17], v[16:17], v[20:21], v[22:23] op_sel_hi:[0,1,1]
	v_xor_b32_e32 v22, 0x80000000, v21
	v_mov_b32_e32 v23, v21
	v_pk_mul_f32 v[22:23], v[14:15], v[22:23] op_sel:[1,0] op_sel_hi:[0,1]
	v_pk_fma_f32 v[20:21], v[14:15], v[20:21], v[22:23] op_sel_hi:[1,0,1]
	v_xor_b32_e32 v22, 0x80000000, v31
	v_mov_b32_e32 v23, v31
	v_pk_mul_f32 v[22:23], v[22:23], v[20:21] op_sel:[0,1] op_sel_hi:[1,0]
	s_nop 0
	v_pk_fma_f32 v[22:23], v[30:31], v[20:21], v[22:23] op_sel_hi:[0,1,1]
	ds_write2_b64 v60, v[16:17], v[22:23] offset0:192 offset1:208
	v_xor_b32_e32 v16, 0x80000000, v21
	v_mov_b32_e32 v17, v21
	v_pk_mul_f32 v[16:17], v[14:15], v[16:17] op_sel:[1,0] op_sel_hi:[0,1]
	v_pk_fma_f32 v[16:17], v[14:15], v[20:21], v[16:17] op_sel_hi:[1,0,1]
	v_xor_b32_e32 v20, 0x80000000, v19
	v_mov_b32_e32 v21, v19
	v_pk_mul_f32 v[20:21], v[20:21], v[16:17] op_sel:[0,1] op_sel_hi:[1,0]
	s_nop 0
	v_pk_fma_f32 v[18:19], v[18:19], v[16:17], v[20:21] op_sel_hi:[0,1,1]
	v_xor_b32_e32 v20, 0x80000000, v17
	v_mov_b32_e32 v21, v17
	v_pk_mul_f32 v[20:21], v[14:15], v[20:21] op_sel:[1,0] op_sel_hi:[0,1]
	v_pk_fma_f32 v[14:15], v[14:15], v[16:17], v[20:21] op_sel_hi:[1,0,1]
	v_xor_b32_e32 v16, 0x80000000, v35
	v_mov_b32_e32 v17, v35
	v_pk_mul_f32 v[16:17], v[16:17], v[14:15] op_sel:[0,1] op_sel_hi:[1,0]
	s_nop 0
	v_pk_fma_f32 v[14:15], v[34:35], v[14:15], v[16:17] op_sel_hi:[0,1,1]
	ds_write2_b64 v13, v[18:19], v[14:15] offset0:224 offset1:240
	v_mov_b32_e32 v14, v1
	v_mov_b32_e32 v10, v178
	v_mov_b32_e32 v13, v177
	s_waitcnt lgkmcnt(0)
	s_barrier
	v_mov_b32_e32 v48, v168
	v_xor_b32_e32 v16, 1, v13
	v_lshlrev_b32_e32 v10, 3, v10
	v_lshlrev_b32_e32 v16, 3, v16
	v_add3_u32 v18, 0, v16, v10
	v_xor_b32_e32 v16, 2, v13
	v_lshlrev_b32_e32 v16, 3, v16
	v_xor_b32_e32 v24, 5, v13
	v_add3_u32 v20, 0, v16, v10
	v_xor_b32_e32 v16, 3, v13
	v_lshlrev_b32_e32 v24, 3, v24
	v_lshlrev_b32_e32 v15, 3, v13
	v_lshlrev_b32_e32 v16, 3, v16
	v_add3_u32 v26, 0, v24, v10
	v_xor_b32_e32 v24, 6, v13
	v_add3_u32 v15, 0, v15, v10
	v_add3_u32 v22, 0, v16, v10
	v_lshlrev_b32_e32 v24, 3, v24
	v_xor_b32_e32 v32, 9, v13
	ds_read_b64 v[16:17], v15
	ds_read_b64 v[18:19], v18
	ds_read_b64 v[20:21], v20
	ds_read_b64 v[22:23], v22
	v_xor_b32_e32 v15, 4, v13
	v_add3_u32 v28, 0, v24, v10
	v_xor_b32_e32 v24, 7, v13
	v_lshlrev_b32_e32 v32, 3, v32
	v_lshlrev_b32_e32 v15, 3, v15
	v_lshlrev_b32_e32 v24, 3, v24
	v_add3_u32 v34, 0, v32, v10
	v_xor_b32_e32 v32, 10, v13
	v_add3_u32 v15, 0, v15, v10
	v_add3_u32 v30, 0, v24, v10
	v_lshlrev_b32_e32 v32, 3, v32
	ds_read_b64 v[24:25], v15
	ds_read_b64 v[26:27], v26
	ds_read_b64 v[28:29], v28
	ds_read_b64 v[30:31], v30
	v_xor_b32_e32 v15, 8, v13
	v_add3_u32 v36, 0, v32, v10
	v_xor_b32_e32 v32, 11, v13
	v_lshlrev_b32_e32 v15, 3, v15
	v_lshlrev_b32_e32 v32, 3, v32
	v_xor_b32_e32 v40, 13, v13
	v_add3_u32 v15, 0, v15, v10
	v_add3_u32 v38, 0, v32, v10
	v_lshlrev_b32_e32 v40, 3, v40
	ds_read_b64 v[32:33], v15
	ds_read_b64 v[34:35], v34
	ds_read_b64 v[36:37], v36
	ds_read_b64 v[38:39], v38
	v_xor_b32_e32 v15, 12, v13
	v_add3_u32 v42, 0, v40, v10
	v_xor_b32_e32 v40, 14, v13
	v_xor_b32_e32 v13, 15, v13
	v_lshlrev_b32_e32 v15, 3, v15
	v_lshlrev_b32_e32 v40, 3, v40
	v_lshlrev_b32_e32 v13, 3, v13
	v_add3_u32 v15, 0, v15, v10
	v_add3_u32 v44, 0, v40, v10
	v_add3_u32 v10, 0, v13, v10
	ds_read_b64 v[40:41], v15
	ds_read_b64 v[42:43], v42
	ds_read_b64 v[44:45], v44
	ds_read_b64 v[46:47], v10
	v_mov_b32_e32 v10, v164
	v_mov_b32_e32 v13, v167
	v_mov_b32_e32 v10, v165
	s_waitcnt lgkmcnt(7)
	v_pk_add_f32 v[52:53], v[16:17], v[32:33]
	v_mov_b32_e32 v10, v166
	v_pk_add_f32 v[16:17], v[16:17], v[32:33] neg_lo:[0,1] neg_hi:[0,1]
	s_waitcnt lgkmcnt(6)
	v_pk_add_f32 v[32:33], v[18:19], v[34:35]
	v_pk_add_f32 v[18:19], v[18:19], v[34:35] neg_lo:[0,1] neg_hi:[0,1]
	v_mov_b32_e32 v13, v169
	v_mov_b32_e32 v50, v170
	v_xor_b32_e32 v34, 0x80000000, v19
	v_mov_b32_e32 v35, v18
	v_ashrrev_i32_e32 v15, 31, v14
	v_pk_mul_f32 v[34:35], v[34:35], v[50:51] op_sel_hi:[1,0] neg_lo:[0,1] neg_hi:[0,1]
	v_mov_b32_e32 v13, v171
	v_pk_fma_f32 v[18:19], v[18:19], v[10:11], v[34:35] op_sel_hi:[1,0,1]
	s_waitcnt lgkmcnt(5)
	v_pk_add_f32 v[34:35], v[20:21], v[36:37]
	v_pk_add_f32 v[20:21], v[20:21], v[36:37] neg_lo:[0,1] neg_hi:[0,1]
	s_mov_b32 s39, 0x8000
	v_xor_b32_e32 v36, 0x80000000, v21
	v_mov_b32_e32 v37, v20
	v_pk_mul_f32 v[36:37], v[36:37], v[48:49] op_sel_hi:[1,0] neg_lo:[0,1] neg_hi:[0,1]
	v_mov_b32_e32 v13, v172
	v_pk_fma_f32 v[20:21], v[20:21], v[48:49], v[36:37] op_sel_hi:[1,0,1]
	s_waitcnt lgkmcnt(4)
	v_pk_add_f32 v[36:37], v[22:23], v[38:39]
	v_pk_add_f32 v[22:23], v[22:23], v[38:39] neg_lo:[0,1] neg_hi:[0,1]
	s_nop 0
	v_pk_mul_f32 v[38:39], v[22:23], v[50:51] op_sel_hi:[1,0]
	v_xor_b32_e32 v54, 0x80000000, v23
	v_mov_b32_e32 v55, v22
	v_pk_fma_f32 v[22:23], v[54:55], v[10:11], v[38:39] op_sel_hi:[1,0,1] neg_lo:[0,1,0] neg_hi:[0,1,0]
	s_waitcnt lgkmcnt(3)
	v_pk_add_f32 v[38:39], v[24:25], v[40:41]
	v_pk_add_f32 v[24:25], v[24:25], v[40:41] neg_lo:[0,1] neg_hi:[0,1]
	v_mov_b32_e32 v13, v177
	v_xor_b32_e32 v41, 0x80000000, v24
	v_mov_b32_e32 v40, v25
	s_waitcnt lgkmcnt(2)
	v_pk_add_f32 v[24:25], v[26:27], v[42:43]
	v_pk_add_f32 v[26:27], v[26:27], v[42:43] neg_lo:[0,1] neg_hi:[0,1]
	s_nop 0
	v_pk_mul_f32 v[42:43], v[26:27], v[50:51] op_sel_hi:[1,0] neg_lo:[0,1] neg_hi:[0,1]
	v_xor_b32_e32 v54, 0x80000000, v27
	v_mov_b32_e32 v55, v26
	v_pk_fma_f32 v[26:27], v[54:55], v[10:11], v[42:43] op_sel_hi:[1,0,1] neg_lo:[0,1,0] neg_hi:[0,1,0]
	s_waitcnt lgkmcnt(1)
	v_pk_add_f32 v[42:43], v[28:29], v[44:45]
	v_pk_add_f32 v[28:29], v[28:29], v[44:45] neg_lo:[0,1] neg_hi:[0,1]
	s_nop 0
	v_xor_b32_e32 v44, 0x80000000, v29
	v_mov_b32_e32 v45, v28
	v_pk_mul_f32 v[44:45], v[44:45], v[48:49] op_sel_hi:[1,0] neg_lo:[0,1] neg_hi:[0,1]
	s_nop 0
	v_pk_fma_f32 v[28:29], v[28:29], v[48:49], v[44:45] op_sel_hi:[1,0,1] neg_lo:[0,1,0] neg_hi:[0,1,0]
	s_waitcnt lgkmcnt(0)
	v_pk_add_f32 v[44:45], v[30:31], v[46:47]
	v_pk_add_f32 v[30:31], v[30:31], v[46:47] neg_lo:[0,1] neg_hi:[0,1]
	s_nop 0
	v_xor_b32_e32 v46, 0x80000000, v31
	v_mov_b32_e32 v47, v30
	v_pk_mul_f32 v[46:47], v[46:47], v[50:51] op_sel_hi:[1,0] neg_lo:[0,1] neg_hi:[0,1]
	v_pk_add_f32 v[50:51], v[32:33], v[24:25]
	v_pk_add_f32 v[24:25], v[32:33], v[24:25] neg_lo:[0,1] neg_hi:[0,1]
	v_pk_fma_f32 v[30:31], v[30:31], v[10:11], v[46:47] op_sel_hi:[1,0,1] neg_lo:[0,1,0] neg_hi:[0,1,0]
	v_xor_b32_e32 v32, 0x80000000, v25
	v_mov_b32_e32 v33, v24
	v_pk_mul_f32 v[32:33], v[32:33], v[48:49] op_sel_hi:[1,0] neg_lo:[0,1] neg_hi:[0,1]
	v_pk_add_f32 v[46:47], v[52:53], v[38:39]
	v_pk_fma_f32 v[24:25], v[24:25], v[48:49], v[32:33] op_sel_hi:[1,0,1]
	v_pk_add_f32 v[32:33], v[34:35], v[42:43]
	v_pk_add_f32 v[34:35], v[34:35], v[42:43] neg_lo:[0,1] neg_hi:[0,1]
	v_pk_add_f32 v[38:39], v[52:53], v[38:39] neg_lo:[0,1] neg_hi:[0,1]
	v_xor_b32_e32 v43, 0x80000000, v34
	v_mov_b32_e32 v42, v35
	v_pk_add_f32 v[34:35], v[36:37], v[44:45]
	v_pk_add_f32 v[36:37], v[36:37], v[44:45] neg_lo:[0,1] neg_hi:[0,1]
	v_mov_b32_e32 v10, v179
	v_xor_b32_e32 v44, 0x80000000, v37
	v_mov_b32_e32 v45, v36
	v_pk_mul_f32 v[44:45], v[44:45], v[48:49] op_sel_hi:[1,0] neg_lo:[0,1] neg_hi:[0,1]
	s_nop 0
	v_pk_fma_f32 v[36:37], v[36:37], v[48:49], v[44:45] op_sel_hi:[1,0,1] neg_lo:[0,1,0] neg_hi:[0,1,0]
	v_pk_add_f32 v[44:45], v[46:47], v[32:33]
	v_pk_add_f32 v[32:33], v[46:47], v[32:33] neg_lo:[0,1] neg_hi:[0,1]
	v_pk_add_f32 v[46:47], v[50:51], v[34:35]
	v_pk_add_f32 v[34:35], v[50:51], v[34:35] neg_lo:[0,1] neg_hi:[0,1]
	s_nop 0
	v_xor_b32_e32 v51, 0x80000000, v34
	v_mov_b32_e32 v50, v35
	v_pk_add_f32 v[34:35], v[44:45], v[46:47]
	v_pk_add_f32 v[44:45], v[44:45], v[46:47] neg_lo:[0,1] neg_hi:[0,1]
	v_pk_add_f32 v[46:47], v[32:33], v[50:51]
	v_pk_add_f32 v[32:33], v[32:33], v[50:51] neg_lo:[0,1] neg_hi:[0,1]
	v_pk_add_f32 v[50:51], v[38:39], v[42:43]
	v_pk_add_f32 v[38:39], v[38:39], v[42:43] neg_lo:[0,1] neg_hi:[0,1]
	v_pk_add_f32 v[42:43], v[24:25], v[36:37]
	v_pk_add_f32 v[24:25], v[24:25], v[36:37] neg_lo:[0,1] neg_hi:[0,1]
	s_nop 0
	v_xor_b32_e32 v37, 0x80000000, v24
	v_mov_b32_e32 v36, v25
	v_pk_add_f32 v[24:25], v[50:51], v[42:43]
	v_pk_add_f32 v[42:43], v[50:51], v[42:43] neg_lo:[0,1] neg_hi:[0,1]
	v_pk_add_f32 v[50:51], v[38:39], v[36:37]
	v_pk_add_f32 v[36:37], v[38:39], v[36:37] neg_lo:[0,1] neg_hi:[0,1]
	v_pk_add_f32 v[38:39], v[16:17], v[40:41]
	v_pk_add_f32 v[16:17], v[16:17], v[40:41] neg_lo:[0,1] neg_hi:[0,1]
	v_pk_add_f32 v[40:41], v[18:19], v[26:27]
	v_pk_add_f32 v[18:19], v[18:19], v[26:27] neg_lo:[0,1] neg_hi:[0,1]
	s_nop 0
	v_xor_b32_e32 v26, 0x80000000, v19
	v_mov_b32_e32 v27, v18
	v_pk_mul_f32 v[26:27], v[48:49], v[26:27] op_sel_hi:[0,1] neg_lo:[1,0] neg_hi:[1,0]
	v_pk_fma_f32 v[18:19], v[48:49], v[18:19], v[26:27] op_sel_hi:[0,1,1]
	v_pk_add_f32 v[26:27], v[20:21], v[28:29]
	v_pk_add_f32 v[20:21], v[20:21], v[28:29] neg_lo:[0,1] neg_hi:[0,1]
	s_nop 0
	v_xor_b32_e32 v29, 0x80000000, v20
	v_mov_b32_e32 v28, v21
	v_pk_add_f32 v[20:21], v[22:23], v[30:31]
	v_pk_add_f32 v[22:23], v[22:23], v[30:31] neg_lo:[0,1] neg_hi:[0,1]
	s_nop 0
	v_xor_b32_e32 v30, 0x80000000, v23
	v_mov_b32_e32 v31, v22
	v_pk_mul_f32 v[30:31], v[48:49], v[30:31] op_sel_hi:[0,1] neg_lo:[1,0] neg_hi:[1,0]
	v_pk_fma_f32 v[22:23], v[48:49], v[22:23], v[30:31] op_sel_hi:[0,1,1] neg_lo:[1,0,0] neg_hi:[1,0,0]
	v_pk_add_f32 v[30:31], v[38:39], v[26:27]
	v_pk_add_f32 v[26:27], v[38:39], v[26:27] neg_lo:[0,1] neg_hi:[0,1]
	v_pk_add_f32 v[38:39], v[40:41], v[20:21]
	v_pk_add_f32 v[20:21], v[40:41], v[20:21] neg_lo:[0,1] neg_hi:[0,1]
	v_mov_b32_e32 v48, v168
	v_xor_b32_e32 v41, 0x80000000, v20
	v_mov_b32_e32 v40, v21
	v_pk_add_f32 v[20:21], v[30:31], v[38:39]
	v_pk_add_f32 v[30:31], v[30:31], v[38:39] neg_lo:[0,1] neg_hi:[0,1]
	v_pk_add_f32 v[38:39], v[26:27], v[40:41]
	v_pk_add_f32 v[26:27], v[26:27], v[40:41] neg_lo:[0,1] neg_hi:[0,1]
	v_pk_add_f32 v[40:41], v[16:17], v[28:29]
	v_pk_add_f32 v[16:17], v[16:17], v[28:29] neg_lo:[0,1] neg_hi:[0,1]
	v_pk_add_f32 v[28:29], v[18:19], v[22:23]
	v_pk_add_f32 v[18:19], v[18:19], v[22:23] neg_lo:[0,1] neg_hi:[0,1]
	s_nop 0
	v_xor_b32_e32 v23, 0x80000000, v18
	v_mov_b32_e32 v22, v19
	v_pk_add_f32 v[18:19], v[40:41], v[28:29]
	v_pk_add_f32 v[28:29], v[40:41], v[28:29] neg_lo:[0,1] neg_hi:[0,1]
	v_pk_add_f32 v[40:41], v[16:17], v[22:23]
	v_pk_add_f32 v[16:17], v[16:17], v[22:23] neg_lo:[0,1] neg_hi:[0,1]
	v_lshl_add_u64 v[22:23], v[14:15], 3, s[48:49]
	global_store_dwordx2 v[22:23], v[34:35], off
	v_add_u32_e32 v22, 0x200, v14
	v_ashrrev_i32_e32 v23, 31, v22
	v_lshl_add_u64 v[22:23], v[22:23], 3, s[48:49]
	global_store_dwordx2 v[22:23], v[20:21], off
	v_add_u32_e32 v20, 0x400, v14
	v_ashrrev_i32_e32 v21, 31, v20
	v_lshl_add_u64 v[20:21], v[20:21], 3, s[48:49]
	global_store_dwordx2 v[20:21], v[24:25], off
	v_add_u32_e32 v20, 0x600, v14
	v_ashrrev_i32_e32 v21, 31, v20
	v_lshl_add_u64 v[20:21], v[20:21], 3, s[48:49]
	global_store_dwordx2 v[20:21], v[18:19], off
	v_add_u32_e32 v18, 0x800, v14
	v_ashrrev_i32_e32 v19, 31, v18
	v_lshl_add_u64 v[18:19], v[18:19], 3, s[48:49]
	global_store_dwordx2 v[18:19], v[46:47], off
	v_add_u32_e32 v18, 0xa00, v14
	v_ashrrev_i32_e32 v19, 31, v18
	v_lshl_add_u64 v[18:19], v[18:19], 3, s[48:49]
	global_store_dwordx2 v[18:19], v[38:39], off
	v_add_u32_e32 v18, 0xc00, v14
	v_ashrrev_i32_e32 v19, 31, v18
	v_lshl_add_u64 v[18:19], v[18:19], 3, s[48:49]
	global_store_dwordx2 v[18:19], v[50:51], off
	v_add_u32_e32 v18, 0xe00, v14
	v_ashrrev_i32_e32 v19, 31, v18
	v_lshl_add_u64 v[18:19], v[18:19], 3, s[48:49]
	global_store_dwordx2 v[18:19], v[40:41], off
	v_add_u32_e32 v18, 0x1000, v14
	v_ashrrev_i32_e32 v19, 31, v18
	v_lshl_add_u64 v[18:19], v[18:19], 3, s[48:49]
	global_store_dwordx2 v[18:19], v[44:45], off
	v_add_u32_e32 v18, 0x1200, v14
	v_ashrrev_i32_e32 v19, 31, v18
	v_lshl_add_u64 v[18:19], v[18:19], 3, s[48:49]
	global_store_dwordx2 v[18:19], v[30:31], off
	v_add_u32_e32 v18, 0x1400, v14
	v_ashrrev_i32_e32 v19, 31, v18
	v_lshl_add_u64 v[18:19], v[18:19], 3, s[48:49]
	global_store_dwordx2 v[18:19], v[42:43], off
	v_add_u32_e32 v18, 0x1600, v14
	v_ashrrev_i32_e32 v19, 31, v18
	v_lshl_add_u64 v[18:19], v[18:19], 3, s[48:49]
	global_store_dwordx2 v[18:19], v[28:29], off
	v_add_u32_e32 v18, 0x1800, v14
	v_ashrrev_i32_e32 v19, 31, v18
	v_lshl_add_u64 v[18:19], v[18:19], 3, s[48:49]
	global_store_dwordx2 v[18:19], v[32:33], off
	v_add_u32_e32 v18, 0x1a00, v14
	v_ashrrev_i32_e32 v19, 31, v18
	v_lshl_add_u64 v[18:19], v[18:19], 3, s[48:49]
	global_store_dwordx2 v[18:19], v[26:27], off
	v_add_u32_e32 v18, 0x1c00, v14
	v_ashrrev_i32_e32 v19, 31, v18
	v_lshl_add_u64 v[18:19], v[18:19], 3, s[48:49]
	global_store_dwordx2 v[18:19], v[36:37], off
	v_add_u32_e32 v18, 0x1e00, v14
	v_ashrrev_i32_e32 v19, 31, v18
	v_lshl_add_u64 v[18:19], v[18:19], 3, s[48:49]
	global_store_dwordx2 v[18:19], v[16:17], off
	v_mov_b32_e32 v50, v170
	v_xor_b32_e32 v16, 1, v13
	v_lshlrev_b32_e32 v10, 3, v10
	v_lshlrev_b32_e32 v16, 3, v16
	v_add3_u32 v18, 0, v16, v10
	v_xor_b32_e32 v16, 2, v13
	v_lshlrev_b32_e32 v16, 3, v16
	v_xor_b32_e32 v24, 5, v13
	v_add3_u32 v20, 0, v16, v10
	v_xor_b32_e32 v16, 3, v13
	v_lshlrev_b32_e32 v24, 3, v24
	v_lshlrev_b32_e32 v15, 3, v13
	v_lshlrev_b32_e32 v16, 3, v16
	v_add3_u32 v26, 0, v24, v10
	v_xor_b32_e32 v24, 6, v13
	v_add3_u32 v15, 0, v15, v10
	v_add3_u32 v22, 0, v16, v10
	v_lshlrev_b32_e32 v24, 3, v24
	v_xor_b32_e32 v32, 9, v13
	ds_read_b64 v[16:17], v15
	ds_read_b64 v[18:19], v18
	ds_read_b64 v[20:21], v20
	ds_read_b64 v[22:23], v22
	v_xor_b32_e32 v15, 4, v13
	v_add3_u32 v28, 0, v24, v10
	v_xor_b32_e32 v24, 7, v13
	v_lshlrev_b32_e32 v32, 3, v32
	v_lshlrev_b32_e32 v15, 3, v15
	v_lshlrev_b32_e32 v24, 3, v24
	v_add3_u32 v34, 0, v32, v10
	v_xor_b32_e32 v32, 10, v13
	v_add3_u32 v15, 0, v15, v10
	v_add3_u32 v30, 0, v24, v10
	v_lshlrev_b32_e32 v32, 3, v32
	ds_read_b64 v[24:25], v15
	ds_read_b64 v[26:27], v26
	ds_read_b64 v[28:29], v28
	ds_read_b64 v[30:31], v30
	v_xor_b32_e32 v15, 8, v13
	v_add3_u32 v36, 0, v32, v10
	v_xor_b32_e32 v32, 11, v13
	v_lshlrev_b32_e32 v15, 3, v15
	v_lshlrev_b32_e32 v32, 3, v32
	v_xor_b32_e32 v40, 13, v13
	v_add3_u32 v15, 0, v15, v10
	v_add3_u32 v38, 0, v32, v10
	v_lshlrev_b32_e32 v40, 3, v40
	ds_read_b64 v[32:33], v15
	ds_read_b64 v[34:35], v34
	ds_read_b64 v[36:37], v36
	ds_read_b64 v[38:39], v38
	v_xor_b32_e32 v15, 12, v13
	v_add3_u32 v42, 0, v40, v10
	v_xor_b32_e32 v40, 14, v13
	v_xor_b32_e32 v13, 15, v13
	v_lshlrev_b32_e32 v15, 3, v15
	v_lshlrev_b32_e32 v40, 3, v40
	v_lshlrev_b32_e32 v13, 3, v13
	v_add3_u32 v15, 0, v15, v10
	v_add3_u32 v44, 0, v40, v10
	v_add3_u32 v10, 0, v13, v10
	ds_read_b64 v[40:41], v15
	ds_read_b64 v[42:43], v42
	ds_read_b64 v[44:45], v44
	ds_read_b64 v[46:47], v10
	v_mov_b32_e32 v10, v164
	v_mov_b32_e32 v13, v167
	v_mov_b32_e32 v10, v165
	s_waitcnt lgkmcnt(7)
	v_pk_add_f32 v[52:53], v[16:17], v[32:33]
	v_mov_b32_e32 v10, v166
	v_pk_add_f32 v[16:17], v[16:17], v[32:33] neg_lo:[0,1] neg_hi:[0,1]
	s_waitcnt lgkmcnt(6)
	v_pk_add_f32 v[32:33], v[18:19], v[34:35]
	v_pk_add_f32 v[18:19], v[18:19], v[34:35] neg_lo:[0,1] neg_hi:[0,1]
	v_mov_b32_e32 v13, v169
	v_xor_b32_e32 v34, 0x80000000, v19
	v_mov_b32_e32 v35, v18
	s_nop 0
	v_pk_mul_f32 v[34:35], v[34:35], v[50:51] op_sel_hi:[1,0] neg_lo:[0,1] neg_hi:[0,1]
	v_mov_b32_e32 v13, v171
	v_pk_fma_f32 v[18:19], v[18:19], v[10:11], v[34:35] op_sel_hi:[1,0,1]
	s_waitcnt lgkmcnt(5)
	v_pk_add_f32 v[34:35], v[20:21], v[36:37]
	v_pk_add_f32 v[20:21], v[20:21], v[36:37] neg_lo:[0,1] neg_hi:[0,1]
	s_nop 0
	v_xor_b32_e32 v36, 0x80000000, v21
	v_mov_b32_e32 v37, v20
	v_pk_mul_f32 v[36:37], v[36:37], v[48:49] op_sel_hi:[1,0] neg_lo:[0,1] neg_hi:[0,1]
	v_mov_b32_e32 v13, v172
	v_pk_fma_f32 v[20:21], v[20:21], v[48:49], v[36:37] op_sel_hi:[1,0,1]
	s_waitcnt lgkmcnt(4)
	v_pk_add_f32 v[36:37], v[22:23], v[38:39]
	v_pk_add_f32 v[22:23], v[22:23], v[38:39] neg_lo:[0,1] neg_hi:[0,1]
	s_nop 0
	v_pk_mul_f32 v[38:39], v[22:23], v[50:51] op_sel_hi:[1,0]
	v_xor_b32_e32 v54, 0x80000000, v23
	v_mov_b32_e32 v55, v22
	v_pk_fma_f32 v[22:23], v[54:55], v[10:11], v[38:39] op_sel_hi:[1,0,1] neg_lo:[0,1,0] neg_hi:[0,1,0]
	s_waitcnt lgkmcnt(3)
	v_pk_add_f32 v[38:39], v[24:25], v[40:41]
	v_pk_add_f32 v[24:25], v[24:25], v[40:41] neg_lo:[0,1] neg_hi:[0,1]
	v_mov_b32_e32 v13, v174
	v_xor_b32_e32 v41, 0x80000000, v24
	v_mov_b32_e32 v40, v25
	s_waitcnt lgkmcnt(2)
	v_pk_add_f32 v[24:25], v[26:27], v[42:43]
	v_pk_add_f32 v[26:27], v[26:27], v[42:43] neg_lo:[0,1] neg_hi:[0,1]
	s_nop 0
	v_pk_mul_f32 v[42:43], v[26:27], v[50:51] op_sel_hi:[1,0] neg_lo:[0,1] neg_hi:[0,1]
	v_xor_b32_e32 v54, 0x80000000, v27
	v_mov_b32_e32 v55, v26
	v_pk_fma_f32 v[26:27], v[54:55], v[10:11], v[42:43] op_sel_hi:[1,0,1] neg_lo:[0,1,0] neg_hi:[0,1,0]
	s_waitcnt lgkmcnt(1)
	v_pk_add_f32 v[42:43], v[28:29], v[44:45]
	v_pk_add_f32 v[28:29], v[28:29], v[44:45] neg_lo:[0,1] neg_hi:[0,1]
	s_nop 0
	v_xor_b32_e32 v44, 0x80000000, v29
	v_mov_b32_e32 v45, v28
	v_pk_mul_f32 v[44:45], v[44:45], v[48:49] op_sel_hi:[1,0] neg_lo:[0,1] neg_hi:[0,1]
	s_nop 0
	v_pk_fma_f32 v[28:29], v[28:29], v[48:49], v[44:45] op_sel_hi:[1,0,1] neg_lo:[0,1,0] neg_hi:[0,1,0]
	s_waitcnt lgkmcnt(0)
	v_pk_add_f32 v[44:45], v[30:31], v[46:47]
	v_pk_add_f32 v[30:31], v[30:31], v[46:47] neg_lo:[0,1] neg_hi:[0,1]
	s_nop 0
	v_xor_b32_e32 v46, 0x80000000, v31
	v_mov_b32_e32 v47, v30
	v_pk_mul_f32 v[46:47], v[46:47], v[50:51] op_sel_hi:[1,0] neg_lo:[0,1] neg_hi:[0,1]
	v_pk_add_f32 v[50:51], v[32:33], v[24:25]
	v_pk_add_f32 v[24:25], v[32:33], v[24:25] neg_lo:[0,1] neg_hi:[0,1]
	v_pk_fma_f32 v[30:31], v[30:31], v[10:11], v[46:47] op_sel_hi:[1,0,1] neg_lo:[0,1,0] neg_hi:[0,1,0]
	v_xor_b32_e32 v32, 0x80000000, v25
	v_mov_b32_e32 v33, v24
	v_pk_mul_f32 v[32:33], v[32:33], v[48:49] op_sel_hi:[1,0] neg_lo:[0,1] neg_hi:[0,1]
	v_pk_add_f32 v[46:47], v[52:53], v[38:39]
	v_pk_fma_f32 v[24:25], v[24:25], v[48:49], v[32:33] op_sel_hi:[1,0,1]
	v_pk_add_f32 v[32:33], v[34:35], v[42:43]
	v_pk_add_f32 v[34:35], v[34:35], v[42:43] neg_lo:[0,1] neg_hi:[0,1]
	v_pk_add_f32 v[38:39], v[52:53], v[38:39] neg_lo:[0,1] neg_hi:[0,1]
	v_xor_b32_e32 v43, 0x80000000, v34
	v_mov_b32_e32 v42, v35
	v_pk_add_f32 v[34:35], v[36:37], v[44:45]
	v_pk_add_f32 v[36:37], v[36:37], v[44:45] neg_lo:[0,1] neg_hi:[0,1]
	v_mov_b32_e32 v10, v184
	v_xor_b32_e32 v44, 0x80000000, v37
	v_mov_b32_e32 v45, v36
	v_pk_mul_f32 v[44:45], v[44:45], v[48:49] op_sel_hi:[1,0] neg_lo:[0,1] neg_hi:[0,1]
	s_nop 0
	v_pk_fma_f32 v[36:37], v[36:37], v[48:49], v[44:45] op_sel_hi:[1,0,1] neg_lo:[0,1,0] neg_hi:[0,1,0]
	v_pk_add_f32 v[44:45], v[46:47], v[32:33]
	v_pk_add_f32 v[32:33], v[46:47], v[32:33] neg_lo:[0,1] neg_hi:[0,1]
	v_pk_add_f32 v[46:47], v[50:51], v[34:35]
	v_pk_add_f32 v[34:35], v[50:51], v[34:35] neg_lo:[0,1] neg_hi:[0,1]
	s_nop 0
	v_xor_b32_e32 v51, 0x80000000, v34
	v_mov_b32_e32 v50, v35
	v_pk_add_f32 v[34:35], v[44:45], v[46:47]
	v_pk_add_f32 v[44:45], v[44:45], v[46:47] neg_lo:[0,1] neg_hi:[0,1]
	v_pk_add_f32 v[46:47], v[32:33], v[50:51]
	v_pk_add_f32 v[32:33], v[32:33], v[50:51] neg_lo:[0,1] neg_hi:[0,1]
	v_pk_add_f32 v[50:51], v[38:39], v[42:43]
	v_pk_add_f32 v[38:39], v[38:39], v[42:43] neg_lo:[0,1] neg_hi:[0,1]
	v_pk_add_f32 v[42:43], v[24:25], v[36:37]
	v_pk_add_f32 v[24:25], v[24:25], v[36:37] neg_lo:[0,1] neg_hi:[0,1]
	s_nop 0
	v_xor_b32_e32 v37, 0x80000000, v24
	v_mov_b32_e32 v36, v25
	v_pk_add_f32 v[24:25], v[50:51], v[42:43]
	v_pk_add_f32 v[42:43], v[50:51], v[42:43] neg_lo:[0,1] neg_hi:[0,1]
	v_pk_add_f32 v[50:51], v[38:39], v[36:37]
	v_pk_add_f32 v[36:37], v[38:39], v[36:37] neg_lo:[0,1] neg_hi:[0,1]
	v_pk_add_f32 v[38:39], v[16:17], v[40:41]
	v_pk_add_f32 v[16:17], v[16:17], v[40:41] neg_lo:[0,1] neg_hi:[0,1]
	v_pk_add_f32 v[40:41], v[18:19], v[26:27]
	v_pk_add_f32 v[18:19], v[18:19], v[26:27] neg_lo:[0,1] neg_hi:[0,1]
	s_nop 0
	v_xor_b32_e32 v26, 0x80000000, v19
	v_mov_b32_e32 v27, v18
	v_pk_mul_f32 v[26:27], v[48:49], v[26:27] op_sel_hi:[0,1] neg_lo:[1,0] neg_hi:[1,0]
	v_pk_fma_f32 v[18:19], v[48:49], v[18:19], v[26:27] op_sel_hi:[0,1,1]
	v_pk_add_f32 v[26:27], v[20:21], v[28:29]
	v_pk_add_f32 v[20:21], v[20:21], v[28:29] neg_lo:[0,1] neg_hi:[0,1]
	s_nop 0
	v_xor_b32_e32 v29, 0x80000000, v20
	v_mov_b32_e32 v28, v21
	v_pk_add_f32 v[20:21], v[22:23], v[30:31]
	v_pk_add_f32 v[22:23], v[22:23], v[30:31] neg_lo:[0,1] neg_hi:[0,1]
	s_nop 0
	v_xor_b32_e32 v30, 0x80000000, v23
	v_mov_b32_e32 v31, v22
	v_pk_mul_f32 v[30:31], v[48:49], v[30:31] op_sel_hi:[0,1] neg_lo:[1,0] neg_hi:[1,0]
	v_pk_fma_f32 v[22:23], v[48:49], v[22:23], v[30:31] op_sel_hi:[0,1,1] neg_lo:[1,0,0] neg_hi:[1,0,0]
	v_pk_add_f32 v[30:31], v[38:39], v[26:27]
	v_pk_add_f32 v[26:27], v[38:39], v[26:27] neg_lo:[0,1] neg_hi:[0,1]
	v_pk_add_f32 v[38:39], v[40:41], v[20:21]
	v_pk_add_f32 v[20:21], v[40:41], v[20:21] neg_lo:[0,1] neg_hi:[0,1]
	s_nop 0
	v_xor_b32_e32 v41, 0x80000000, v20
	v_mov_b32_e32 v40, v21
	v_pk_add_f32 v[20:21], v[30:31], v[38:39]
	v_pk_add_f32 v[30:31], v[30:31], v[38:39] neg_lo:[0,1] neg_hi:[0,1]
	v_pk_add_f32 v[38:39], v[26:27], v[40:41]
	v_pk_add_f32 v[26:27], v[26:27], v[40:41] neg_lo:[0,1] neg_hi:[0,1]
	v_pk_add_f32 v[40:41], v[16:17], v[28:29]
	v_pk_add_f32 v[16:17], v[16:17], v[28:29] neg_lo:[0,1] neg_hi:[0,1]
	v_pk_add_f32 v[28:29], v[18:19], v[22:23]
	v_pk_add_f32 v[18:19], v[18:19], v[22:23] neg_lo:[0,1] neg_hi:[0,1]
	s_nop 0
	v_xor_b32_e32 v23, 0x80000000, v18
	v_mov_b32_e32 v22, v19
	v_pk_add_f32 v[18:19], v[40:41], v[28:29]
	v_pk_add_f32 v[28:29], v[40:41], v[28:29] neg_lo:[0,1] neg_hi:[0,1]
	v_pk_add_f32 v[40:41], v[16:17], v[22:23]
	v_pk_add_f32 v[16:17], v[16:17], v[22:23] neg_lo:[0,1] neg_hi:[0,1]
	v_add_u32_e32 v22, 0x2000, v14
	v_ashrrev_i32_e32 v23, 31, v22
	v_lshl_add_u64 v[22:23], v[22:23], 3, s[48:49]
	global_store_dwordx2 v[22:23], v[34:35], off
	v_add_u32_e32 v22, 0x2200, v14
	v_ashrrev_i32_e32 v23, 31, v22
	v_lshl_add_u64 v[22:23], v[22:23], 3, s[48:49]
	global_store_dwordx2 v[22:23], v[20:21], off
	v_add_u32_e32 v20, 0x2400, v14
	v_ashrrev_i32_e32 v21, 31, v20
	v_lshl_add_u64 v[20:21], v[20:21], 3, s[48:49]
	global_store_dwordx2 v[20:21], v[24:25], off
	v_add_u32_e32 v20, 0x2600, v14
	v_ashrrev_i32_e32 v21, 31, v20
	v_lshl_add_u64 v[20:21], v[20:21], 3, s[48:49]
	global_store_dwordx2 v[20:21], v[18:19], off
	v_add_u32_e32 v18, 0x2800, v14
	v_ashrrev_i32_e32 v19, 31, v18
	v_lshl_add_u64 v[18:19], v[18:19], 3, s[48:49]
	global_store_dwordx2 v[18:19], v[46:47], off
	v_add_u32_e32 v18, 0x2a00, v14
	v_ashrrev_i32_e32 v19, 31, v18
	v_lshl_add_u64 v[18:19], v[18:19], 3, s[48:49]
	global_store_dwordx2 v[18:19], v[38:39], off
	v_add_u32_e32 v18, 0x2c00, v14
	v_ashrrev_i32_e32 v19, 31, v18
	v_lshl_add_u64 v[18:19], v[18:19], 3, s[48:49]
	global_store_dwordx2 v[18:19], v[50:51], off
	v_add_u32_e32 v18, 0x2e00, v14
	v_ashrrev_i32_e32 v19, 31, v18
	v_lshl_add_u64 v[18:19], v[18:19], 3, s[48:49]
	global_store_dwordx2 v[18:19], v[40:41], off
	v_add_u32_e32 v18, 0x3000, v14
	v_ashrrev_i32_e32 v19, 31, v18
	v_lshl_add_u64 v[18:19], v[18:19], 3, s[48:49]
	global_store_dwordx2 v[18:19], v[44:45], off
	v_add_u32_e32 v18, 0x3200, v14
	v_ashrrev_i32_e32 v19, 31, v18
	v_lshl_add_u64 v[18:19], v[18:19], 3, s[48:49]
	global_store_dwordx2 v[18:19], v[30:31], off
	v_add_u32_e32 v18, 0x3400, v14
	v_ashrrev_i32_e32 v19, 31, v18
	v_lshl_add_u64 v[18:19], v[18:19], 3, s[48:49]
	global_store_dwordx2 v[18:19], v[42:43], off
	v_add_u32_e32 v18, 0x3600, v14
	v_ashrrev_i32_e32 v19, 31, v18
	v_lshl_add_u64 v[18:19], v[18:19], 3, s[48:49]
	global_store_dwordx2 v[18:19], v[28:29], off
	v_add_u32_e32 v18, 0x3800, v14
	v_ashrrev_i32_e32 v19, 31, v18
	v_lshl_add_u64 v[18:19], v[18:19], 3, s[48:49]
	global_store_dwordx2 v[18:19], v[32:33], off
	v_add_u32_e32 v18, 0x3a00, v14
	v_ashrrev_i32_e32 v19, 31, v18
	v_lshl_add_u64 v[18:19], v[18:19], 3, s[48:49]
	global_store_dwordx2 v[18:19], v[26:27], off
	v_add_u32_e32 v18, 0x3c00, v14
	v_add_u32_e32 v14, 0x3e00, v14
	v_ashrrev_i32_e32 v15, 31, v14
	v_ashrrev_i32_e32 v19, 31, v18
	v_lshl_add_u64 v[14:15], v[14:15], 3, s[48:49]
	v_lshl_add_u64 v[18:19], v[18:19], 3, s[48:49]
	global_store_dwordx2 v[14:15], v[16:17], off
	v_mov_b32_e32 v16, v185
	v_mov_b32_e32 v14, v1
	global_store_dwordx2 v[18:19], v[36:37], off
	s_barrier
	s_nop 0
	v_pk_mul_f32 v[36:37], v[16:17], s[66:67] op_sel_hi:[0,1] neg_lo:[1,0]
	s_mov_b64 s[66:67], vcc
	v_ashrrev_i32_e32 v15, 31, v14
	v_lshl_add_u64 v[18:19], v[14:15], 2, s[66:67]
	v_add_co_u32_e32 v28, vcc, s85, v18
	v_pk_mul_f32 v[52:53], v[16:17], s[60:61] op_sel_hi:[0,1] neg_lo:[1,0]
	s_nop 0
	v_addc_co_u32_e32 v29, vcc, 0, v19, vcc
	v_add_co_u32_e32 v20, vcc, s84, v18
	s_movk_i32 s61, 0x3000
	s_nop 0
	v_addc_co_u32_e32 v21, vcc, 0, v19, vcc
	v_add_co_u32_e32 v48, vcc, s61, v18
	v_pk_mul_f32 v[54:55], v[16:17], s[94:95] op_sel_hi:[0,1] neg_lo:[1,0]
	s_nop 0
	v_addc_co_u32_e32 v49, vcc, 0, v19, vcc
	v_add_co_u32_e32 v22, vcc, s45, v18
	v_pk_mul_f32 v[82:83], v[16:17], s[68:69] op_sel_hi:[0,1] neg_lo:[1,0]
	s_nop 0
	v_addc_co_u32_e32 v23, vcc, 0, v19, vcc
	v_add_co_u32_e32 v58, vcc, s86, v18
	s_mov_b32 s68, 0x3f7ec46d
	s_nop 0
	v_addc_co_u32_e32 v59, vcc, 0, v19, vcc
	v_add_co_u32_e32 v60, vcc, s88, v18
	v_pk_mul_f32 v[32:33], v[16:17], s[78:79] op_sel_hi:[0,1] neg_lo:[1,0]
	s_nop 0
	v_addc_co_u32_e32 v61, vcc, 0, v19, vcc
	v_add_co_u32_e32 v66, vcc, s90, v18
	v_pk_mul_f32 v[40:41], v[16:17], s[80:81] op_sel_hi:[0,1] neg_lo:[1,0]
	s_nop 0
	v_addc_co_u32_e32 v67, vcc, 0, v19, vcc
	v_add_co_u32_e32 v68, vcc, s39, v18
	s_mov_b32 s39, 0x9000
	s_nop 0
	v_addc_co_u32_e32 v69, vcc, 0, v19, vcc
	v_add_co_u32_e32 v24, vcc, s39, v18
	s_mov_b32 s39, 0xb000
	s_nop 0
	v_addc_co_u32_e32 v25, vcc, 0, v19, vcc
	v_add_co_u32_e32 v26, vcc, s91, v18
	s_mov_b32 s80, 0x3f54db31
	s_nop 0
	v_addc_co_u32_e32 v27, vcc, 0, v19, vcc
	v_add_co_u32_e32 v34, vcc, s39, v18
	s_mov_b32 s39, 0xc000
	s_nop 0
	v_addc_co_u32_e32 v35, vcc, 0, v19, vcc
	v_add_co_u32_e32 v38, vcc, s39, v18
	s_mov_b32 s39, 0xd000
	s_nop 0
	v_addc_co_u32_e32 v39, vcc, 0, v19, vcc
	v_add_co_u32_e32 v46, vcc, s39, v18
	s_mov_b32 s39, 0xe000
	s_nop 0
	v_addc_co_u32_e32 v47, vcc, 0, v19, vcc
	v_add_co_u32_e32 v50, vcc, s39, v18
	s_mov_b32 s39, 0xf000
	s_nop 0
	v_addc_co_u32_e32 v51, vcc, 0, v19, vcc
	v_add_co_u32_e32 v70, vcc, s39, v18
	s_mov_b32 s69, 0xbdc8bd36
	s_nop 0
	v_addc_co_u32_e32 v71, vcc, 0, v19, vcc
	global_load_dword v90, v[68:69], off
	global_load_dword v92, v[68:69], off offset:2048
	global_load_dword v94, v[26:27], off offset:-4096
	global_load_dword v96, v[24:25], off offset:2048
	global_load_dword v98, v[26:27], off
	global_load_dword v100, v[26:27], off offset:2048
	global_load_dword v102, v[38:39], off offset:-4096
	global_load_dword v104, v[34:35], off offset:2048
	global_load_dword v106, v[38:39], off
	global_load_dword v108, v[38:39], off offset:2048
	global_load_dword v110, v[50:51], off offset:-4096
	global_load_dword v112, v[46:47], off offset:2048
	global_load_dword v114, v[50:51], off
	global_load_dword v116, v[50:51], off offset:2048
	global_load_dword v118, v[70:71], off
	global_load_dword v56, v[20:21], off
	s_nop 0
	global_load_dword v50, v[20:21], off offset:2048
	global_load_dword v120, v[70:71], off offset:2048
	global_load_dword v46, v[22:23], off offset:-4096
	global_load_dword v38, v[22:23], off
	global_load_dword v74, v[20:21], off offset:-4096
	global_load_dword v34, v[22:23], off offset:2048
	global_load_dword v26, v[60:61], off offset:-4096
	global_load_dword v24, v[60:61], off
	s_nop 0
	global_load_dword v22, v[60:61], off offset:2048
	global_load_dword v20, v[68:69], off offset:-4096
	s_nop 0
	global_load_dword v68, v[18:19], off
	global_load_dword v76, v[18:19], off offset:2048
	global_load_dword v72, v[28:29], off offset:2048
	s_nop 0
	global_load_dword v48, v[48:49], off offset:2048
	s_nop 0
	global_load_dword v28, v[58:59], off offset:2048
	global_load_dword v18, v[66:67], off offset:2048
	s_mov_b32 s88, 0x3e47c5c2
	v_pk_fma_f32 v[58:59], v[10:11], s[74:75], v[54:55] op_sel_hi:[0,1,1]
	s_mov_b32 s74, 0x3f226799
	s_mov_b32 s81, 0xbf0e39da
	v_pk_mul_f32 v[42:43], v[16:17], s[52:53] op_sel_hi:[0,1] neg_lo:[1,0]
	v_pk_mul_f32 v[64:65], v[16:17], s[62:63] op_sel_hi:[0,1] neg_lo:[1,0]
	s_mov_b32 s89, 0xbf7b14be
	v_pk_fma_f32 v[124:125], v[10:11], s[68:69], v[32:33] op_sel_hi:[0,1,1]
	s_mov_b32 s75, 0xbf45e403
	s_mov_b32 s52, 0x3f3504f3
	v_pk_mul_f32 v[32:33], v[16:17], s[30:31] op_sel_hi:[0,1] neg_lo:[1,0]
	s_mov_b32 s30, 0x3dc8bd36
	v_pk_mul_f32 v[62:63], v[16:17], s[56:57] op_sel_hi:[0,1] neg_lo:[1,0]
	v_pk_fma_f32 v[60:61], v[10:11], s[80:81], v[52:53] op_sel_hi:[0,1,1]
	s_mov_b32 s53, 0xbf3504f3
	v_pk_fma_f32 v[52:53], v[10:11], s[74:75], v[64:65] op_sel_hi:[0,1,1]
	s_mov_b32 s31, 0xbf7ec46d
	v_pk_fma_f32 v[64:65], v[10:11], s[88:89], v[32:33] op_sel_hi:[0,1,1]
	v_pk_mul_f32 v[32:33], v[16:17], s[34:35] op_sel_hi:[0,1] neg_lo:[1,0]
	s_mov_b32 s78, 0x3f61c598
	v_pk_fma_f32 v[54:55], v[10:11], s[52:53], v[62:63] op_sel_hi:[0,1,1]
	v_pk_fma_f32 v[62:63], v[10:11], s[30:31], v[32:33] op_sel_hi:[0,1,1]
	v_pk_mul_f32 v[32:33], v[16:17], s[36:37] op_sel_hi:[0,1] neg_lo:[1,0]
	s_mov_b32 s79, 0xbef15aea
	v_pk_mul_f32 v[44:45], v[16:17], s[50:51] op_sel_hi:[0,1] neg_lo:[1,0]
	v_pk_fma_f32 v[32:33], v[10:11], s[76:77], v[32:33] op_sel_hi:[0,1,1]
	s_mov_b32 s94, 0x3f6c835e
	v_pk_fma_f32 v[66:67], v[10:11], s[78:79], v[44:45] op_sel_hi:[0,1,1]
	v_pk_fma_f32 v[44:45], v[10:11], s[82:83], v[82:83] op_sel_hi:[0,1,1]
	s_mov_b32 s82, 0x3ef15aea
	s_mov_b32 s95, 0xbec3ef15
	v_pk_mul_f32 v[84:85], v[16:17], s[70:71] op_sel_hi:[0,1] neg_lo:[1,0]
	s_mov_b32 s83, 0xbf61c598
	v_pk_mul_f32 v[30:31], v[16:17], s[40:41] op_sel_hi:[0,1] neg_lo:[1,0]
	s_mov_b32 s84, 0x3ec3ef15
	s_mov_b32 s40, 0x3f74fa0b
	v_pk_fma_f32 v[70:71], v[10:11], s[94:95], v[42:43] op_sel_hi:[0,1,1]
	v_pk_fma_f32 v[42:43], v[10:11], s[82:83], v[84:85] op_sel_hi:[0,1,1]
	s_mov_b32 s85, 0xbf6c835e
	s_mov_b32 s41, 0xbe94a031
	v_pk_mul_f32 v[86:87], v[16:17], s[58:59] op_sel_hi:[0,1] neg_lo:[1,0]
	s_mov_b32 s86, 0x3e94a031
	v_pk_fma_f32 v[78:79], v[10:11], s[40:41], v[40:41] op_sel_hi:[0,1,1]
	v_pk_fma_f32 v[40:41], v[10:11], s[84:85], v[86:87] op_sel_hi:[0,1,1]
	s_mov_b32 s87, 0xbf74fa0b
	v_pk_mul_f32 v[88:89], v[16:17], s[64:65] op_sel_hi:[0,1] neg_lo:[1,0]
	v_pk_fma_f32 v[122:123], v[10:11], s[46:47], v[30:31] op_sel_hi:[0,1,1]
	v_pk_fma_f32 v[30:31], v[10:11], s[86:87], v[88:89] op_sel_hi:[0,1,1]
	s_waitcnt vmcnt(31)
	v_pk_mul_f32 v[82:83], v[32:33], v[90:91] op_sel_hi:[1,0]
	v_pk_mul_f32 v[32:33], v[16:17], s[2:3] op_sel_hi:[0,1] neg_lo:[1,0]
	v_pk_fma_f32 v[32:33], v[10:11], s[0:1], v[32:33] op_sel_hi:[0,1,1]
	s_waitcnt vmcnt(30)
	v_pk_mul_f32 v[84:85], v[32:33], v[92:93] op_sel_hi:[1,0]
	v_pk_mul_f32 v[32:33], v[16:17], s[6:7] op_sel_hi:[0,1] neg_lo:[1,0]
	v_pk_fma_f32 v[32:33], v[10:11], s[4:5], v[32:33] op_sel_hi:[0,1,1]
	s_waitcnt vmcnt(29)
	v_pk_mul_f32 v[86:87], v[32:33], v[94:95] op_sel_hi:[1,0]
	v_pk_mul_f32 v[32:33], v[16:17], s[10:11] op_sel_hi:[0,1] neg_lo:[1,0]
	v_pk_fma_f32 v[32:33], v[10:11], s[8:9], v[32:33] op_sel_hi:[0,1,1]
	s_waitcnt vmcnt(28)
	v_pk_mul_f32 v[88:89], v[32:33], v[96:97] op_sel_hi:[1,0]
	v_pk_mul_f32 v[32:33], v[16:17], s[16:17] op_sel_hi:[0,1] neg_lo:[1,0]
	v_pk_fma_f32 v[32:33], v[10:11], s[12:13], v[32:33] op_sel_hi:[0,1,1]
	s_waitcnt vmcnt(27)
	v_pk_mul_f32 v[90:91], v[32:33], v[98:99] op_sel_hi:[1,0]
	v_pk_mul_f32 v[32:33], v[16:17], s[20:21] op_sel_hi:[0,1] neg_lo:[1,0]
	v_pk_fma_f32 v[32:33], v[10:11], s[18:19], v[32:33] op_sel_hi:[0,1,1]
	s_waitcnt vmcnt(26)
	v_pk_mul_f32 v[92:93], v[32:33], v[100:101] op_sel_hi:[1,0]
	v_pk_mul_f32 v[32:33], v[16:17], s[24:25] op_sel_hi:[0,1] neg_lo:[1,0]
	v_pk_fma_f32 v[32:33], v[10:11], s[22:23], v[32:33] op_sel_hi:[0,1,1]
	s_waitcnt vmcnt(25)
	v_pk_mul_f32 v[94:95], v[32:33], v[102:103] op_sel_hi:[1,0]
	v_pk_mul_f32 v[32:33], v[16:17], s[28:29] op_sel_hi:[0,1] neg_lo:[1,0]
	v_pk_fma_f32 v[32:33], v[10:11], s[26:27], v[32:33] op_sel_hi:[0,1,1]
	s_waitcnt vmcnt(24)
	v_pk_mul_f32 v[96:97], v[32:33], v[104:105] op_sel_hi:[1,0]
	v_pk_mul_f32 v[32:33], v[16:17], s[52:53] op_sel_hi:[0,0] neg_lo:[1,0]
	v_pk_fma_f32 v[32:33], v[10:11], s[38:39], v[32:33] op_sel_hi:[0,0,1] neg_lo:[0,0,1] neg_hi:[0,0,1]
	s_waitcnt vmcnt(23)
	v_pk_mul_f32 v[98:99], v[32:33], v[106:107] op_sel_hi:[1,0]
	v_pk_mul_f32 v[32:33], v[16:17], s[26:27] op_sel_hi:[0,1] neg_lo:[1,0]
	v_pk_fma_f32 v[32:33], v[10:11], s[28:29], v[32:33] op_sel_hi:[0,1,1]
	s_waitcnt vmcnt(22)
	v_pk_mul_f32 v[100:101], v[32:33], v[108:109] op_sel_hi:[1,0]
	v_pk_mul_f32 v[32:33], v[16:17], s[22:23] op_sel_hi:[0,1] neg_lo:[1,0]
	v_pk_fma_f32 v[32:33], v[10:11], s[24:25], v[32:33] op_sel_hi:[0,1,1]
	s_waitcnt vmcnt(21)
	v_pk_mul_f32 v[102:103], v[32:33], v[110:111] op_sel_hi:[1,0]
	v_pk_mul_f32 v[32:33], v[16:17], s[18:19] op_sel_hi:[0,1] neg_lo:[1,0]
	v_pk_fma_f32 v[32:33], v[10:11], s[20:21], v[32:33] op_sel_hi:[0,1,1]
	s_waitcnt vmcnt(20)
	v_pk_mul_f32 v[104:105], v[32:33], v[112:113] op_sel_hi:[1,0]
	v_pk_mul_f32 v[32:33], v[16:17], s[12:13] op_sel_hi:[0,1] neg_lo:[1,0]
	v_pk_fma_f32 v[32:33], v[10:11], s[16:17], v[32:33] op_sel_hi:[0,1,1]
	s_waitcnt vmcnt(19)
	v_pk_mul_f32 v[106:107], v[32:33], v[114:115] op_sel_hi:[1,0]
	v_pk_mul_f32 v[32:33], v[16:17], s[8:9] op_sel_hi:[0,1] neg_lo:[1,0]
	v_pk_fma_f32 v[32:33], v[10:11], s[10:11], v[32:33] op_sel_hi:[0,1,1]
	s_mov_b32 s70, 0x3f7b14be
	s_waitcnt vmcnt(18)
	v_pk_mul_f32 v[108:109], v[32:33], v[116:117] op_sel_hi:[1,0]
	v_pk_mul_f32 v[32:33], v[16:17], s[4:5] op_sel_hi:[0,1] neg_lo:[1,0]
	v_pk_mul_f32 v[16:17], v[16:17], s[0:1] op_sel_hi:[0,1] neg_lo:[1,0]
	s_mov_b32 s71, 0xbe47c5c2
	v_pk_fma_f32 v[16:17], v[10:11], s[2:3], v[16:17] op_sel_hi:[0,1,1]
	v_pk_fma_f32 v[80:81], v[10:11], s[70:71], v[36:37] op_sel_hi:[0,1,1]
	v_pk_fma_f32 v[32:33], v[10:11], s[6:7], v[32:33] op_sel_hi:[0,1,1]
	s_waitcnt vmcnt(14)
	v_pk_mul_f32 v[112:113], v[16:17], v[120:121] op_sel_hi:[1,0]
	v_mov_b32_e32 v16, v180
	v_mov_b32_e32 v17, v181
	v_mov_b32_e32 v10, v164
	s_waitcnt vmcnt(5)
	v_pk_fma_f32 v[126:127], v[68:69], v[122:123], v[82:83] op_sel_hi:[0,1,1]
	v_pk_fma_f32 v[68:69], v[68:69], v[122:123], v[82:83] op_sel_hi:[0,1,1] neg_lo:[0,0,1] neg_hi:[0,0,1]
	s_waitcnt vmcnt(4)
	v_pk_fma_f32 v[82:83], v[124:125], v[76:77], v[84:85] op_sel_hi:[1,0,1]
	v_pk_fma_f32 v[76:77], v[124:125], v[76:77], v[84:85] op_sel_hi:[1,0,1] neg_lo:[0,0,1] neg_hi:[0,0,1]
	v_pk_mul_f32 v[110:111], v[32:33], v[118:119] op_sel_hi:[1,0]
	v_mov_b32_e32 v114, v165
	v_mov_b32_e32 v32, v166
	v_mov_b32_e32 v116, v167
	v_mov_b32_e32 v10, v168
	v_mov_b32_e32 v118, v169
	v_mov_b32_e32 v36, v170
	v_mov_b32_e32 v120, v171
	v_xor_b32_e32 v84, 0x80000000, v77
	v_mov_b32_e32 v85, v76
	v_mov_b32_e32 v15, v172
	v_pk_mul_f32 v[84:85], v[84:85], v[120:121] op_sel_hi:[1,0] neg_lo:[0,1] neg_hi:[0,1]
	s_nop 0
	v_pk_fma_f32 v[76:77], v[76:77], v[114:115], v[84:85] op_sel_hi:[1,0,1]
	v_pk_fma_f32 v[84:85], v[80:81], v[74:75], v[86:87] op_sel_hi:[1,0,1]
	v_pk_fma_f32 v[74:75], v[80:81], v[74:75], v[86:87] op_sel_hi:[1,0,1] neg_lo:[0,0,1] neg_hi:[0,0,1]
	s_nop 0
	v_xor_b32_e32 v80, 0x80000000, v75
	v_mov_b32_e32 v81, v74
	v_pk_mul_f32 v[80:81], v[80:81], v[36:37] op_sel_hi:[1,0] neg_lo:[0,1] neg_hi:[0,1]
	s_nop 0
	v_pk_fma_f32 v[74:75], v[74:75], v[32:33], v[80:81] op_sel_hi:[1,0,1]
	s_waitcnt vmcnt(3)
	v_pk_fma_f32 v[80:81], v[78:79], v[72:73], v[88:89] op_sel_hi:[1,0,1]
	v_pk_fma_f32 v[72:73], v[78:79], v[72:73], v[88:89] op_sel_hi:[1,0,1] neg_lo:[0,0,1] neg_hi:[0,0,1]
	s_nop 0
	v_xor_b32_e32 v78, 0x80000000, v73
	v_mov_b32_e32 v79, v72
	v_pk_mul_f32 v[78:79], v[78:79], v[118:119] op_sel_hi:[1,0] neg_lo:[0,1] neg_hi:[0,1]
	s_nop 0
	v_pk_fma_f32 v[72:73], v[72:73], v[116:117], v[78:79] op_sel_hi:[1,0,1]
	v_pk_fma_f32 v[78:79], v[70:71], v[56:57], v[90:91] op_sel_hi:[1,0,1]
	v_pk_fma_f32 v[56:57], v[70:71], v[56:57], v[90:91] op_sel_hi:[1,0,1] neg_lo:[0,0,1] neg_hi:[0,0,1]
	s_nop 0
	v_xor_b32_e32 v70, 0x80000000, v57
	v_mov_b32_e32 v71, v56
	v_pk_mul_f32 v[70:71], v[70:71], v[10:11] op_sel_hi:[1,0] neg_lo:[0,1] neg_hi:[0,1]
	s_nop 0
	v_pk_fma_f32 v[56:57], v[56:57], v[10:11], v[70:71] op_sel_hi:[1,0,1]
	v_pk_fma_f32 v[70:71], v[66:67], v[50:51], v[92:93] op_sel_hi:[1,0,1]
	v_pk_fma_f32 v[50:51], v[66:67], v[50:51], v[92:93] op_sel_hi:[1,0,1] neg_lo:[0,0,1] neg_hi:[0,0,1]
	s_nop 0
	v_pk_mul_f32 v[66:67], v[50:51], v[118:119] op_sel_hi:[1,0]
	v_xor_b32_e32 v86, 0x80000000, v51
	v_mov_b32_e32 v87, v50
	v_pk_fma_f32 v[50:51], v[60:61], v[46:47], v[94:95] op_sel_hi:[1,0,1]
	v_pk_fma_f32 v[46:47], v[60:61], v[46:47], v[94:95] op_sel_hi:[1,0,1] neg_lo:[0,0,1] neg_hi:[0,0,1]
	v_pk_fma_f32 v[66:67], v[86:87], v[116:117], v[66:67] op_sel_hi:[1,0,1] neg_lo:[0,1,0] neg_hi:[0,1,0]
	v_pk_mul_f32 v[60:61], v[46:47], v[36:37] op_sel_hi:[1,0]
	v_xor_b32_e32 v86, 0x80000000, v47
	v_mov_b32_e32 v87, v46
	s_waitcnt vmcnt(2)
	v_pk_fma_f32 v[46:47], v[58:59], v[48:49], v[96:97] op_sel_hi:[1,0,1]
	v_pk_fma_f32 v[48:49], v[58:59], v[48:49], v[96:97] op_sel_hi:[1,0,1] neg_lo:[0,0,1] neg_hi:[0,0,1]
	v_pk_fma_f32 v[60:61], v[86:87], v[32:33], v[60:61] op_sel_hi:[1,0,1] neg_lo:[0,1,0] neg_hi:[0,1,0]
	v_pk_mul_f32 v[58:59], v[48:49], v[120:121] op_sel_hi:[1,0]
	v_xor_b32_e32 v86, 0x80000000, v49
	v_mov_b32_e32 v87, v48
	v_pk_fma_f32 v[48:49], v[86:87], v[114:115], v[58:59] op_sel_hi:[1,0,1] neg_lo:[0,1,0] neg_hi:[0,1,0]
	v_pk_fma_f32 v[58:59], v[54:55], v[38:39], v[98:99] op_sel_hi:[1,0,1]
	v_pk_fma_f32 v[38:39], v[54:55], v[38:39], v[98:99] op_sel_hi:[1,0,1] neg_lo:[0,0,1] neg_hi:[0,0,1]
	s_nop 0
	v_xor_b32_e32 v55, 0x80000000, v38
	v_mov_b32_e32 v54, v39
	v_pk_fma_f32 v[38:39], v[52:53], v[34:35], v[100:101] op_sel_hi:[1,0,1]
	v_pk_fma_f32 v[34:35], v[52:53], v[34:35], v[100:101] op_sel_hi:[1,0,1] neg_lo:[0,0,1] neg_hi:[0,0,1]
	s_nop 0
	v_pk_mul_f32 v[52:53], v[34:35], v[120:121] op_sel_hi:[1,0] neg_lo:[0,1] neg_hi:[0,1]
	v_xor_b32_e32 v86, 0x80000000, v35
	v_mov_b32_e32 v87, v34
	v_pk_fma_f32 v[34:35], v[44:45], v[26:27], v[102:103] op_sel_hi:[1,0,1]
	v_pk_fma_f32 v[26:27], v[44:45], v[26:27], v[102:103] op_sel_hi:[1,0,1] neg_lo:[0,0,1] neg_hi:[0,0,1]
	v_pk_fma_f32 v[52:53], v[86:87], v[114:115], v[52:53] op_sel_hi:[1,0,1] neg_lo:[0,1,0] neg_hi:[0,1,0]
	v_pk_mul_f32 v[44:45], v[26:27], v[36:37] op_sel_hi:[1,0] neg_lo:[0,1] neg_hi:[0,1]
	v_xor_b32_e32 v86, 0x80000000, v27
	v_mov_b32_e32 v87, v26
	s_waitcnt vmcnt(1)
	v_pk_fma_f32 v[26:27], v[42:43], v[28:29], v[104:105] op_sel_hi:[1,0,1]
	v_pk_fma_f32 v[28:29], v[42:43], v[28:29], v[104:105] op_sel_hi:[1,0,1] neg_lo:[0,0,1] neg_hi:[0,0,1]
	v_pk_fma_f32 v[86:87], v[86:87], v[32:33], v[44:45] op_sel_hi:[1,0,1] neg_lo:[0,1,0] neg_hi:[0,1,0]
	v_pk_mul_f32 v[42:43], v[28:29], v[118:119] op_sel_hi:[1,0] neg_lo:[0,1] neg_hi:[0,1]
	v_xor_b32_e32 v44, 0x80000000, v29
	v_mov_b32_e32 v45, v28
	v_pk_fma_f32 v[28:29], v[40:41], v[24:25], v[106:107] op_sel_hi:[1,0,1]
	v_pk_fma_f32 v[24:25], v[40:41], v[24:25], v[106:107] op_sel_hi:[1,0,1] neg_lo:[0,0,1] neg_hi:[0,0,1]
	v_pk_fma_f32 v[42:43], v[44:45], v[116:117], v[42:43] op_sel_hi:[1,0,1] neg_lo:[0,1,0] neg_hi:[0,1,0]
	v_xor_b32_e32 v40, 0x80000000, v25
	v_mov_b32_e32 v41, v24
	v_pk_mul_f32 v[40:41], v[40:41], v[10:11] op_sel_hi:[1,0] neg_lo:[0,1] neg_hi:[0,1]
	v_pk_add_f32 v[44:45], v[126:127], v[58:59] neg_lo:[0,1] neg_hi:[0,1]
	v_pk_fma_f32 v[88:89], v[24:25], v[10:11], v[40:41] op_sel_hi:[1,0,1] neg_lo:[0,1,0] neg_hi:[0,1,0]
	v_pk_fma_f32 v[24:25], v[30:31], v[22:23], v[108:109] op_sel_hi:[1,0,1]
	v_pk_fma_f32 v[22:23], v[30:31], v[22:23], v[108:109] op_sel_hi:[1,0,1] neg_lo:[0,0,1] neg_hi:[0,0,1]
	s_nop 0
	v_xor_b32_e32 v30, 0x80000000, v23
	v_mov_b32_e32 v31, v22
	v_pk_mul_f32 v[30:31], v[30:31], v[118:119] op_sel_hi:[1,0] neg_lo:[0,1] neg_hi:[0,1]
	s_nop 0
	v_pk_fma_f32 v[90:91], v[22:23], v[116:117], v[30:31] op_sel_hi:[1,0,1] neg_lo:[0,1,0] neg_hi:[0,1,0]
	v_pk_fma_f32 v[22:23], v[64:65], v[20:21], v[110:111] op_sel_hi:[1,0,1]
	v_pk_fma_f32 v[20:21], v[64:65], v[20:21], v[110:111] op_sel_hi:[1,0,1] neg_lo:[0,0,1] neg_hi:[0,0,1]
	s_nop 0
	v_xor_b32_e32 v30, 0x80000000, v21
	v_mov_b32_e32 v31, v20
	v_pk_mul_f32 v[30:31], v[30:31], v[36:37] op_sel_hi:[1,0] neg_lo:[0,1] neg_hi:[0,1]
	s_nop 0
	v_pk_fma_f32 v[64:65], v[20:21], v[32:33], v[30:31] op_sel_hi:[1,0,1] neg_lo:[0,1,0] neg_hi:[0,1,0]
	s_waitcnt vmcnt(0)
	v_pk_fma_f32 v[20:21], v[62:63], v[18:19], v[112:113] op_sel_hi:[1,0,1]
	v_pk_fma_f32 v[18:19], v[62:63], v[18:19], v[112:113] op_sel_hi:[1,0,1] neg_lo:[0,0,1] neg_hi:[0,0,1]
	s_nop 0
	v_xor_b32_e32 v30, 0x80000000, v19
	v_mov_b32_e32 v31, v18
	v_pk_mul_f32 v[30:31], v[30:31], v[120:121] op_sel_hi:[1,0] neg_lo:[0,1] neg_hi:[0,1]
	s_nop 0
	v_pk_fma_f32 v[62:63], v[18:19], v[114:115], v[30:31] op_sel_hi:[1,0,1] neg_lo:[0,1,0] neg_hi:[0,1,0]
	v_pk_add_f32 v[30:31], v[82:83], v[38:39]
	v_pk_add_f32 v[38:39], v[82:83], v[38:39] neg_lo:[0,1] neg_hi:[0,1]
	v_pk_add_f32 v[18:19], v[126:127], v[58:59]
	v_xor_b32_e32 v40, 0x80000000, v39
	v_mov_b32_e32 v41, v38
	v_pk_mul_f32 v[40:41], v[40:41], v[36:37] op_sel_hi:[1,0] neg_lo:[0,1] neg_hi:[0,1]
	s_nop 0
	v_pk_fma_f32 v[38:39], v[38:39], v[32:33], v[40:41] op_sel_hi:[1,0,1]
	v_pk_add_f32 v[40:41], v[84:85], v[34:35]
	v_pk_add_f32 v[34:35], v[84:85], v[34:35] neg_lo:[0,1] neg_hi:[0,1]
	s_nop 0
	v_xor_b32_e32 v58, 0x80000000, v35
	v_mov_b32_e32 v59, v34
	v_pk_mul_f32 v[58:59], v[58:59], v[10:11] op_sel_hi:[1,0] neg_lo:[0,1] neg_hi:[0,1]
	s_nop 0
	v_pk_fma_f32 v[34:35], v[34:35], v[10:11], v[58:59] op_sel_hi:[1,0,1]
	v_pk_add_f32 v[58:59], v[80:81], v[26:27]
	v_pk_add_f32 v[26:27], v[80:81], v[26:27] neg_lo:[0,1] neg_hi:[0,1]
	s_nop 0
	v_pk_mul_f32 v[80:81], v[26:27], v[36:37] op_sel_hi:[1,0]
	v_xor_b32_e32 v82, 0x80000000, v27
	v_mov_b32_e32 v83, v26
	v_pk_add_f32 v[26:27], v[78:79], v[28:29]
	v_pk_add_f32 v[28:29], v[78:79], v[28:29] neg_lo:[0,1] neg_hi:[0,1]
	v_pk_fma_f32 v[80:81], v[82:83], v[32:33], v[80:81] op_sel_hi:[1,0,1] neg_lo:[0,1,0] neg_hi:[0,1,0]
	v_xor_b32_e32 v79, 0x80000000, v28
	v_mov_b32_e32 v78, v29
	v_pk_add_f32 v[28:29], v[70:71], v[24:25]
	v_pk_add_f32 v[24:25], v[70:71], v[24:25] neg_lo:[0,1] neg_hi:[0,1]
	s_nop 0
	v_pk_mul_f32 v[70:71], v[24:25], v[36:37] op_sel_hi:[1,0] neg_lo:[0,1] neg_hi:[0,1]
	v_xor_b32_e32 v82, 0x80000000, v25
	v_mov_b32_e32 v83, v24
	v_pk_fma_f32 v[24:25], v[82:83], v[32:33], v[70:71] op_sel_hi:[1,0,1] neg_lo:[0,1,0] neg_hi:[0,1,0]
	v_pk_add_f32 v[70:71], v[50:51], v[22:23]
	v_pk_add_f32 v[22:23], v[50:51], v[22:23] neg_lo:[0,1] neg_hi:[0,1]
	s_nop 0
	v_xor_b32_e32 v50, 0x80000000, v23
	v_mov_b32_e32 v51, v22
	v_pk_mul_f32 v[50:51], v[50:51], v[10:11] op_sel_hi:[1,0] neg_lo:[0,1] neg_hi:[0,1]
	s_nop 0
	v_pk_fma_f32 v[50:51], v[22:23], v[10:11], v[50:51] op_sel_hi:[1,0,1] neg_lo:[0,1,0] neg_hi:[0,1,0]
	v_pk_add_f32 v[22:23], v[46:47], v[20:21]
	v_pk_add_f32 v[20:21], v[46:47], v[20:21] neg_lo:[0,1] neg_hi:[0,1]
	s_nop 0
	v_xor_b32_e32 v46, 0x80000000, v21
	v_mov_b32_e32 v47, v20
	v_pk_mul_f32 v[46:47], v[46:47], v[36:37] op_sel_hi:[1,0] neg_lo:[0,1] neg_hi:[0,1]
	s_nop 0
	v_pk_fma_f32 v[20:21], v[20:21], v[32:33], v[46:47] op_sel_hi:[1,0,1] neg_lo:[0,1,0] neg_hi:[0,1,0]
	v_pk_add_f32 v[46:47], v[18:19], v[26:27]
	v_pk_add_f32 v[18:19], v[18:19], v[26:27] neg_lo:[0,1] neg_hi:[0,1]
	v_pk_add_f32 v[26:27], v[30:31], v[28:29]
	v_pk_add_f32 v[28:29], v[30:31], v[28:29] neg_lo:[0,1] neg_hi:[0,1]
	s_nop 0
	v_xor_b32_e32 v30, 0x80000000, v29
	v_mov_b32_e32 v31, v28
	v_pk_mul_f32 v[30:31], v[30:31], v[10:11] op_sel_hi:[1,0] neg_lo:[0,1] neg_hi:[0,1]
	s_nop 0
	v_pk_fma_f32 v[28:29], v[28:29], v[10:11], v[30:31] op_sel_hi:[1,0,1]
	v_pk_add_f32 v[30:31], v[40:41], v[70:71]
	v_pk_add_f32 v[40:41], v[40:41], v[70:71] neg_lo:[0,1] neg_hi:[0,1]
	v_pk_add_f32 v[82:83], v[46:47], v[30:31] neg_lo:[0,1] neg_hi:[0,1]
	v_xor_b32_e32 v71, 0x80000000, v40
	v_mov_b32_e32 v70, v41
	v_pk_add_f32 v[40:41], v[58:59], v[22:23]
	v_pk_add_f32 v[22:23], v[58:59], v[22:23] neg_lo:[0,1] neg_hi:[0,1]
	s_nop 0
	v_xor_b32_e32 v58, 0x80000000, v23
	v_mov_b32_e32 v59, v22
	v_pk_mul_f32 v[58:59], v[58:59], v[10:11] op_sel_hi:[1,0] neg_lo:[0,1] neg_hi:[0,1]
	s_nop 0
	v_pk_fma_f32 v[58:59], v[22:23], v[10:11], v[58:59] op_sel_hi:[1,0,1] neg_lo:[0,1,0] neg_hi:[0,1,0]
	v_pk_add_f32 v[22:23], v[46:47], v[30:31]
	v_pk_add_f32 v[30:31], v[26:27], v[40:41]
	v_pk_add_f32 v[26:27], v[26:27], v[40:41] neg_lo:[0,1] neg_hi:[0,1]
	v_pk_add_f32 v[84:85], v[22:23], v[30:31]
	v_xor_b32_e32 v41, 0x80000000, v26
	v_mov_b32_e32 v40, v27
	v_pk_add_f32 v[30:31], v[22:23], v[30:31] neg_lo:[0,1] neg_hi:[0,1]
	v_pk_add_f32 v[46:47], v[82:83], v[40:41]
	v_pk_add_f32 v[22:23], v[82:83], v[40:41] neg_lo:[0,1] neg_hi:[0,1]
	v_pk_add_f32 v[40:41], v[28:29], v[58:59]
	v_pk_add_f32 v[28:29], v[28:29], v[58:59] neg_lo:[0,1] neg_hi:[0,1]
	v_pk_add_f32 v[26:27], v[18:19], v[70:71]
	v_pk_add_f32 v[18:19], v[18:19], v[70:71] neg_lo:[0,1] neg_hi:[0,1]
	v_xor_b32_e32 v59, 0x80000000, v28
	v_mov_b32_e32 v58, v29
	v_pk_add_f32 v[70:71], v[26:27], v[40:41]
	v_pk_add_f32 v[26:27], v[26:27], v[40:41] neg_lo:[0,1] neg_hi:[0,1]
	v_pk_add_f32 v[40:41], v[18:19], v[58:59]
	v_pk_add_f32 v[18:19], v[18:19], v[58:59] neg_lo:[0,1] neg_hi:[0,1]
	v_pk_add_f32 v[58:59], v[38:39], v[24:25]
	v_pk_add_f32 v[24:25], v[38:39], v[24:25] neg_lo:[0,1] neg_hi:[0,1]
	v_pk_add_f32 v[28:29], v[44:45], v[78:79]
	v_xor_b32_e32 v38, 0x80000000, v25
	v_mov_b32_e32 v39, v24
	v_pk_mul_f32 v[38:39], v[10:11], v[38:39] op_sel_hi:[0,1] neg_lo:[1,0] neg_hi:[1,0]
	v_pk_fma_f32 v[38:39], v[10:11], v[24:25], v[38:39] op_sel_hi:[0,1,1]
	v_pk_add_f32 v[24:25], v[34:35], v[50:51]
	v_pk_add_f32 v[34:35], v[34:35], v[50:51] neg_lo:[0,1] neg_hi:[0,1]
	v_pk_add_f32 v[44:45], v[44:45], v[78:79] neg_lo:[0,1] neg_hi:[0,1]
	v_xor_b32_e32 v79, 0x80000000, v34
	v_mov_b32_e32 v78, v35
	v_pk_add_f32 v[34:35], v[80:81], v[20:21]
	v_pk_add_f32 v[20:21], v[80:81], v[20:21] neg_lo:[0,1] neg_hi:[0,1]
	s_nop 0
	v_xor_b32_e32 v50, 0x80000000, v21
	v_mov_b32_e32 v51, v20
	v_pk_mul_f32 v[50:51], v[10:11], v[50:51] op_sel_hi:[0,1] neg_lo:[1,0] neg_hi:[1,0]
	v_pk_fma_f32 v[20:21], v[10:11], v[20:21], v[50:51] op_sel_hi:[0,1,1] neg_lo:[1,0,0] neg_hi:[1,0,0]
	v_pk_add_f32 v[50:51], v[28:29], v[24:25]
	v_pk_add_f32 v[24:25], v[28:29], v[24:25] neg_lo:[0,1] neg_hi:[0,1]
	v_pk_add_f32 v[28:29], v[58:59], v[34:35]
	v_pk_add_f32 v[34:35], v[58:59], v[34:35] neg_lo:[0,1] neg_hi:[0,1]
	v_pk_add_f32 v[80:81], v[50:51], v[28:29]
	v_xor_b32_e32 v59, 0x80000000, v34
	v_mov_b32_e32 v58, v35
	v_pk_add_f32 v[34:35], v[50:51], v[28:29] neg_lo:[0,1] neg_hi:[0,1]
	v_pk_add_f32 v[50:51], v[24:25], v[58:59]
	v_pk_add_f32 v[24:25], v[24:25], v[58:59] neg_lo:[0,1] neg_hi:[0,1]
	v_pk_add_f32 v[28:29], v[44:45], v[78:79]
	v_pk_add_f32 v[58:59], v[44:45], v[78:79] neg_lo:[0,1] neg_hi:[0,1]
	v_pk_add_f32 v[44:45], v[38:39], v[20:21]
	v_pk_add_f32 v[20:21], v[38:39], v[20:21] neg_lo:[0,1] neg_hi:[0,1]
	v_pk_add_f32 v[78:79], v[28:29], v[44:45]
	v_xor_b32_e32 v39, 0x80000000, v20
	v_mov_b32_e32 v38, v21
	v_pk_add_f32 v[28:29], v[28:29], v[44:45] neg_lo:[0,1] neg_hi:[0,1]
	v_pk_add_f32 v[44:45], v[58:59], v[38:39]
	v_pk_add_f32 v[20:21], v[58:59], v[38:39] neg_lo:[0,1] neg_hi:[0,1]
	v_pk_add_f32 v[38:39], v[68:69], v[54:55]
	v_pk_add_f32 v[58:59], v[68:69], v[54:55] neg_lo:[0,1] neg_hi:[0,1]
	v_pk_add_f32 v[54:55], v[76:77], v[52:53]
	v_pk_add_f32 v[52:53], v[76:77], v[52:53] neg_lo:[0,1] neg_hi:[0,1]
	s_nop 0
	v_xor_b32_e32 v68, 0x80000000, v53
	v_mov_b32_e32 v69, v52
	v_pk_mul_f32 v[68:69], v[36:37], v[68:69] op_sel_hi:[0,1] neg_lo:[1,0] neg_hi:[1,0]
	v_pk_fma_f32 v[52:53], v[32:33], v[52:53], v[68:69] op_sel_hi:[0,1,1]
	v_pk_add_f32 v[68:69], v[74:75], v[86:87]
	v_pk_add_f32 v[74:75], v[74:75], v[86:87] neg_lo:[0,1] neg_hi:[0,1]
	s_nop 0
	v_xor_b32_e32 v76, 0x80000000, v75
	v_mov_b32_e32 v77, v74
	v_pk_mul_f32 v[76:77], v[10:11], v[76:77] op_sel_hi:[0,1] neg_lo:[1,0] neg_hi:[1,0]
	v_pk_fma_f32 v[74:75], v[10:11], v[74:75], v[76:77] op_sel_hi:[0,1,1]
	v_pk_add_f32 v[76:77], v[72:73], v[42:43]
	v_pk_add_f32 v[42:43], v[72:73], v[42:43] neg_lo:[0,1] neg_hi:[0,1]
	s_nop 0
	v_xor_b32_e32 v72, 0x80000000, v43
	v_mov_b32_e32 v73, v42
	v_pk_mul_f32 v[72:73], v[32:33], v[72:73] op_sel_hi:[0,1] neg_lo:[1,0] neg_hi:[1,0]
	v_pk_fma_f32 v[42:43], v[36:37], v[42:43], v[72:73] op_sel_hi:[0,1,1]
	v_pk_add_f32 v[72:73], v[56:57], v[88:89]
	v_pk_add_f32 v[56:57], v[56:57], v[88:89] neg_lo:[0,1] neg_hi:[0,1]
	s_nop 0
	v_xor_b32_e32 v83, 0x80000000, v56
	v_mov_b32_e32 v82, v57
	v_pk_add_f32 v[56:57], v[66:67], v[90:91]
	v_pk_add_f32 v[66:67], v[66:67], v[90:91] neg_lo:[0,1] neg_hi:[0,1]
	s_nop 0
	v_xor_b32_e32 v86, 0x80000000, v67
	v_mov_b32_e32 v87, v66
	v_pk_mul_f32 v[86:87], v[32:33], v[86:87] op_sel_hi:[0,1] neg_lo:[1,0] neg_hi:[1,0]
	v_pk_fma_f32 v[66:67], v[36:37], v[66:67], v[86:87] op_sel_hi:[0,1,1] neg_lo:[1,0,0] neg_hi:[1,0,0]
	v_pk_add_f32 v[86:87], v[60:61], v[64:65]
	v_pk_add_f32 v[60:61], v[60:61], v[64:65] neg_lo:[0,1] neg_hi:[0,1]
	s_nop 0
	v_xor_b32_e32 v64, 0x80000000, v61
	v_mov_b32_e32 v65, v60
	v_pk_mul_f32 v[64:65], v[10:11], v[64:65] op_sel_hi:[0,1] neg_lo:[1,0] neg_hi:[1,0]
	v_pk_fma_f32 v[60:61], v[10:11], v[60:61], v[64:65] op_sel_hi:[0,1,1] neg_lo:[1,0,0] neg_hi:[1,0,0]
	v_pk_add_f32 v[64:65], v[48:49], v[62:63]
	v_pk_add_f32 v[48:49], v[48:49], v[62:63] neg_lo:[0,1] neg_hi:[0,1]
	s_nop 0
	v_xor_b32_e32 v62, 0x80000000, v49
	v_mov_b32_e32 v63, v48
	v_pk_mul_f32 v[36:37], v[36:37], v[62:63] op_sel_hi:[0,1] neg_lo:[1,0] neg_hi:[1,0]
	v_pk_fma_f32 v[36:37], v[32:33], v[48:49], v[36:37] op_sel_hi:[0,1,1] neg_lo:[1,0,0] neg_hi:[1,0,0]
	v_pk_add_f32 v[32:33], v[38:39], v[72:73]
	v_pk_add_f32 v[48:49], v[38:39], v[72:73] neg_lo:[0,1] neg_hi:[0,1]
	v_pk_add_f32 v[38:39], v[56:57], v[54:55]
	v_pk_add_f32 v[54:55], v[54:55], v[56:57] neg_lo:[0,1] neg_hi:[0,1]
	v_pk_add_f32 v[62:63], v[68:69], v[86:87] neg_lo:[0,1] neg_hi:[0,1]
	v_xor_b32_e32 v56, 0x80000000, v55
	v_mov_b32_e32 v57, v54
	v_pk_mul_f32 v[56:57], v[10:11], v[56:57] op_sel_hi:[0,1] neg_lo:[1,0] neg_hi:[1,0]
	v_pk_fma_f32 v[56:57], v[10:11], v[54:55], v[56:57] op_sel_hi:[0,1,1]
	v_pk_add_f32 v[54:55], v[68:69], v[86:87]
	v_xor_b32_e32 v69, 0x80000000, v62
	v_mov_b32_e32 v68, v63
	v_pk_add_f32 v[62:63], v[76:77], v[64:65]
	v_pk_add_f32 v[64:65], v[76:77], v[64:65] neg_lo:[0,1] neg_hi:[0,1]
	s_nop 0
	v_xor_b32_e32 v72, 0x80000000, v65
	v_mov_b32_e32 v73, v64
	v_pk_mul_f32 v[72:73], v[10:11], v[72:73] op_sel_hi:[0,1] neg_lo:[1,0] neg_hi:[1,0]
	v_pk_fma_f32 v[64:65], v[10:11], v[64:65], v[72:73] op_sel_hi:[0,1,1] neg_lo:[1,0,0] neg_hi:[1,0,0]
	v_pk_add_f32 v[72:73], v[32:33], v[54:55]
	v_pk_add_f32 v[32:33], v[32:33], v[54:55] neg_lo:[0,1] neg_hi:[0,1]
	v_pk_add_f32 v[54:55], v[38:39], v[62:63]
	v_pk_add_f32 v[38:39], v[38:39], v[62:63] neg_lo:[0,1] neg_hi:[0,1]
	v_pk_add_f32 v[76:77], v[72:73], v[54:55]
	v_xor_b32_e32 v63, 0x80000000, v38
	v_mov_b32_e32 v62, v39
	v_pk_add_f32 v[54:55], v[72:73], v[54:55] neg_lo:[0,1] neg_hi:[0,1]
	v_pk_add_f32 v[72:73], v[32:33], v[62:63]
	v_pk_add_f32 v[38:39], v[32:33], v[62:63] neg_lo:[0,1] neg_hi:[0,1]
	v_pk_add_f32 v[32:33], v[48:49], v[68:69]
	v_pk_add_f32 v[62:63], v[48:49], v[68:69] neg_lo:[0,1] neg_hi:[0,1]
	v_pk_add_f32 v[48:49], v[56:57], v[64:65]
	v_pk_add_f32 v[56:57], v[56:57], v[64:65] neg_lo:[0,1] neg_hi:[0,1]
	s_nop 0
	v_xor_b32_e32 v65, 0x80000000, v56
	v_mov_b32_e32 v64, v57
	v_pk_add_f32 v[56:57], v[32:33], v[48:49]
	v_pk_add_f32 v[48:49], v[32:33], v[48:49] neg_lo:[0,1] neg_hi:[0,1]
	v_pk_add_f32 v[68:69], v[62:63], v[64:65]
	v_pk_add_f32 v[32:33], v[62:63], v[64:65] neg_lo:[0,1] neg_hi:[0,1]
	v_pk_add_f32 v[64:65], v[66:67], v[52:53]
	v_pk_add_f32 v[52:53], v[52:53], v[66:67] neg_lo:[0,1] neg_hi:[0,1]
	v_pk_add_f32 v[62:63], v[58:59], v[82:83]
	v_xor_b32_e32 v66, 0x80000000, v53
	v_mov_b32_e32 v67, v52
	v_pk_mul_f32 v[66:67], v[10:11], v[66:67] op_sel_hi:[0,1] neg_lo:[1,0] neg_hi:[1,0]
	v_pk_fma_f32 v[52:53], v[10:11], v[52:53], v[66:67] op_sel_hi:[0,1,1]
	v_pk_add_f32 v[66:67], v[74:75], v[60:61]
	v_pk_add_f32 v[60:61], v[74:75], v[60:61] neg_lo:[0,1] neg_hi:[0,1]
	v_pk_add_f32 v[58:59], v[58:59], v[82:83] neg_lo:[0,1] neg_hi:[0,1]
	v_xor_b32_e32 v75, 0x80000000, v60
	v_mov_b32_e32 v74, v61
	v_pk_add_f32 v[60:61], v[42:43], v[36:37]
	v_pk_add_f32 v[36:37], v[42:43], v[36:37] neg_lo:[0,1] neg_hi:[0,1]
	s_nop 0
	v_xor_b32_e32 v42, 0x80000000, v37
	v_mov_b32_e32 v43, v36
	v_pk_mul_f32 v[42:43], v[10:11], v[42:43] op_sel_hi:[0,1] neg_lo:[1,0] neg_hi:[1,0]
	v_pk_fma_f32 v[36:37], v[10:11], v[36:37], v[42:43] op_sel_hi:[0,1,1] neg_lo:[1,0,0] neg_hi:[1,0,0]
	v_pk_add_f32 v[42:43], v[62:63], v[66:67]
	v_pk_add_f32 v[62:63], v[62:63], v[66:67] neg_lo:[0,1] neg_hi:[0,1]
	v_pk_add_f32 v[66:67], v[64:65], v[60:61]
	v_pk_add_f32 v[60:61], v[64:65], v[60:61] neg_lo:[0,1] neg_hi:[0,1]
	v_lshl_add_u32 v10, v13, 3, 0
	v_xor_b32_e32 v65, 0x80000000, v60
	v_mov_b32_e32 v64, v61
	v_pk_add_f32 v[60:61], v[42:43], v[66:67]
	v_pk_add_f32 v[66:67], v[42:43], v[66:67] neg_lo:[0,1] neg_hi:[0,1]
	v_pk_add_f32 v[82:83], v[62:63], v[64:65]
	v_pk_add_f32 v[42:43], v[62:63], v[64:65] neg_lo:[0,1] neg_hi:[0,1]
	v_pk_add_f32 v[64:65], v[52:53], v[36:37]
	v_pk_add_f32 v[36:37], v[52:53], v[36:37] neg_lo:[0,1] neg_hi:[0,1]
	v_pk_add_f32 v[62:63], v[58:59], v[74:75]
	v_pk_add_f32 v[58:59], v[58:59], v[74:75] neg_lo:[0,1] neg_hi:[0,1]
	v_xor_b32_e32 v75, 0x80000000, v36
	v_mov_b32_e32 v74, v37
	v_pk_add_f32 v[86:87], v[62:63], v[64:65]
	v_pk_add_f32 v[52:53], v[62:63], v[64:65] neg_lo:[0,1] neg_hi:[0,1]
	v_pk_add_f32 v[62:63], v[58:59], v[74:75]
	v_pk_add_f32 v[36:37], v[58:59], v[74:75] neg_lo:[0,1] neg_hi:[0,1]
	v_xor_b32_e32 v58, 0x80000000, v85
	v_mov_b32_e32 v59, v85
	v_pk_mul_f32 v[58:59], v[58:59], s[14:15]
	v_xor_b32_e32 v64, 0x80000000, v77
	v_pk_fma_f32 v[58:59], v[84:85], s[42:43], v[58:59] op_sel_hi:[0,1,1]
	ds_write_b64 v10, v[58:59]
	v_pk_fma_f32 v[58:59], v[16:17], s[92:93], v[16:17] op_sel:[1,0,0] op_sel_hi:[0,1,1]
	v_mov_b32_e32 v65, v77
	v_pk_mul_f32 v[64:65], v[58:59], v[64:65] op_sel:[1,0] op_sel_hi:[0,1]
	v_pk_fma_f32 v[64:65], v[58:59], v[76:77], v[64:65] op_sel_hi:[1,0,1]
	ds_write_b64 v10, v[64:65] offset:4224
	v_xor_b32_e32 v64, 0x80000000, v59
	v_mov_b32_e32 v65, v59
	v_pk_mul_f32 v[64:65], v[16:17], v[64:65] op_sel:[1,0] op_sel_hi:[0,1]
	v_pk_fma_f32 v[58:59], v[16:17], v[58:59], v[64:65] op_sel_hi:[1,0,1]
	v_xor_b32_e32 v64, 0x80000000, v81
	v_mov_b32_e32 v65, v81
	v_pk_mul_f32 v[64:65], v[58:59], v[64:65] op_sel:[1,0] op_sel_hi:[0,1]
	v_pk_fma_f32 v[64:65], v[58:59], v[80:81], v[64:65] op_sel_hi:[1,0,1]
	ds_write_b64 v10, v[64:65] offset:8448
	v_xor_b32_e32 v64, 0x80000000, v59
	v_mov_b32_e32 v65, v59
	v_pk_mul_f32 v[64:65], v[16:17], v[64:65] op_sel:[1,0] op_sel_hi:[0,1]
	v_pk_fma_f32 v[58:59], v[16:17], v[58:59], v[64:65] op_sel_hi:[1,0,1]
	v_xor_b32_e32 v64, 0x80000000, v61
	v_mov_b32_e32 v65, v61
	v_pk_mul_f32 v[64:65], v[58:59], v[64:65] op_sel:[1,0] op_sel_hi:[0,1]
	v_pk_fma_f32 v[60:61], v[58:59], v[60:61], v[64:65] op_sel_hi:[1,0,1]
	ds_write_b64 v10, v[60:61] offset:12672
	v_xor_b32_e32 v60, 0x80000000, v59
	v_mov_b32_e32 v61, v59
	v_pk_mul_f32 v[60:61], v[16:17], v[60:61] op_sel:[1,0] op_sel_hi:[0,1]
	v_pk_fma_f32 v[58:59], v[16:17], v[58:59], v[60:61] op_sel_hi:[1,0,1]
	v_xor_b32_e32 v60, 0x80000000, v71
	v_mov_b32_e32 v61, v71
	v_pk_mul_f32 v[60:61], v[60:61], v[58:59] op_sel:[0,1] op_sel_hi:[1,0]
	s_nop 0
	v_pk_fma_f32 v[60:61], v[70:71], v[58:59], v[60:61] op_sel_hi:[0,1,1]
	ds_write_b64 v10, v[60:61] offset:16896
	v_xor_b32_e32 v60, 0x80000000, v59
	v_mov_b32_e32 v61, v59
	v_pk_mul_f32 v[60:61], v[16:17], v[60:61] op_sel:[1,0] op_sel_hi:[0,1]
	v_pk_fma_f32 v[58:59], v[16:17], v[58:59], v[60:61] op_sel_hi:[1,0,1]
	v_xor_b32_e32 v60, 0x80000000, v57
	v_mov_b32_e32 v61, v57
	v_pk_mul_f32 v[60:61], v[58:59], v[60:61] op_sel:[1,0] op_sel_hi:[0,1]
	v_pk_fma_f32 v[56:57], v[58:59], v[56:57], v[60:61] op_sel_hi:[1,0,1]
	ds_write_b64 v10, v[56:57] offset:21120
	v_xor_b32_e32 v56, 0x80000000, v59
	v_mov_b32_e32 v57, v59
	v_pk_mul_f32 v[56:57], v[16:17], v[56:57] op_sel:[1,0] op_sel_hi:[0,1]
	v_pk_fma_f32 v[56:57], v[16:17], v[58:59], v[56:57] op_sel_hi:[1,0,1]
	v_xor_b32_e32 v58, 0x80000000, v79
	v_mov_b32_e32 v59, v79
	v_pk_mul_f32 v[58:59], v[58:59], v[56:57] op_sel:[0,1] op_sel_hi:[1,0]
	s_nop 0
	v_pk_fma_f32 v[58:59], v[78:79], v[56:57], v[58:59] op_sel_hi:[0,1,1]
	ds_write_b64 v10, v[58:59] offset:25344
	v_xor_b32_e32 v58, 0x80000000, v57
	v_mov_b32_e32 v59, v57
	v_pk_mul_f32 v[58:59], v[16:17], v[58:59] op_sel:[1,0] op_sel_hi:[0,1]
	v_pk_fma_f32 v[56:57], v[16:17], v[56:57], v[58:59] op_sel_hi:[1,0,1]
	v_xor_b32_e32 v58, 0x80000000, v87
	v_mov_b32_e32 v59, v87
	v_pk_mul_f32 v[58:59], v[58:59], v[56:57] op_sel:[0,1] op_sel_hi:[1,0]
	s_nop 0
	v_pk_fma_f32 v[58:59], v[86:87], v[56:57], v[58:59] op_sel_hi:[0,1,1]
	ds_write_b64 v10, v[58:59] offset:29568
	v_xor_b32_e32 v58, 0x80000000, v57
	v_mov_b32_e32 v59, v57
	v_pk_mul_f32 v[58:59], v[16:17], v[58:59] op_sel:[1,0] op_sel_hi:[0,1]
	v_pk_fma_f32 v[56:57], v[16:17], v[56:57], v[58:59] op_sel_hi:[1,0,1]
	v_xor_b32_e32 v58, 0x80000000, v47
	v_mov_b32_e32 v59, v47
	v_pk_mul_f32 v[58:59], v[58:59], v[56:57] op_sel:[0,1] op_sel_hi:[1,0]
	s_nop 0
	v_pk_fma_f32 v[46:47], v[46:47], v[56:57], v[58:59] op_sel_hi:[0,1,1]
	ds_write_b64 v10, v[46:47] offset:33792
	v_xor_b32_e32 v46, 0x80000000, v57
	v_mov_b32_e32 v47, v57
	v_pk_mul_f32 v[46:47], v[16:17], v[46:47] op_sel:[1,0] op_sel_hi:[0,1]
	v_pk_fma_f32 v[46:47], v[16:17], v[56:57], v[46:47] op_sel_hi:[1,0,1]
	v_xor_b32_e32 v56, 0x80000000, v73
	v_mov_b32_e32 v57, v73
	v_pk_mul_f32 v[56:57], v[56:57], v[46:47] op_sel:[0,1] op_sel_hi:[1,0]
	s_nop 0
	v_pk_fma_f32 v[56:57], v[72:73], v[46:47], v[56:57] op_sel_hi:[0,1,1]
	ds_write_b64 v10, v[56:57] offset:38016
	v_xor_b32_e32 v56, 0x80000000, v47
	v_mov_b32_e32 v57, v47
	v_pk_mul_f32 v[56:57], v[16:17], v[56:57] op_sel:[1,0] op_sel_hi:[0,1]
	v_pk_fma_f32 v[46:47], v[16:17], v[46:47], v[56:57] op_sel_hi:[1,0,1]
	v_xor_b32_e32 v56, 0x80000000, v51
	v_mov_b32_e32 v57, v51
	v_pk_mul_f32 v[56:57], v[56:57], v[46:47] op_sel:[0,1] op_sel_hi:[1,0]
	s_nop 0
	v_pk_fma_f32 v[50:51], v[50:51], v[46:47], v[56:57] op_sel_hi:[0,1,1]
	ds_write_b64 v10, v[50:51] offset:42240
	v_xor_b32_e32 v50, 0x80000000, v47
	v_mov_b32_e32 v51, v47
	v_pk_mul_f32 v[50:51], v[16:17], v[50:51] op_sel:[1,0] op_sel_hi:[0,1]
	v_pk_fma_f32 v[46:47], v[16:17], v[46:47], v[50:51] op_sel_hi:[1,0,1]
	v_xor_b32_e32 v50, 0x80000000, v83
	v_mov_b32_e32 v51, v83
	v_pk_mul_f32 v[50:51], v[50:51], v[46:47] op_sel:[0,1] op_sel_hi:[1,0]
	s_nop 0
	v_pk_fma_f32 v[50:51], v[82:83], v[46:47], v[50:51] op_sel_hi:[0,1,1]
	ds_write_b64 v10, v[50:51] offset:46464
	v_xor_b32_e32 v50, 0x80000000, v47
	v_mov_b32_e32 v51, v47
	v_pk_mul_f32 v[50:51], v[16:17], v[50:51] op_sel:[1,0] op_sel_hi:[0,1]
	v_pk_fma_f32 v[46:47], v[16:17], v[46:47], v[50:51] op_sel_hi:[1,0,1]
	v_xor_b32_e32 v50, 0x80000000, v41
	v_mov_b32_e32 v51, v41
	v_pk_mul_f32 v[50:51], v[50:51], v[46:47] op_sel:[0,1] op_sel_hi:[1,0]
	s_nop 0
	v_pk_fma_f32 v[40:41], v[40:41], v[46:47], v[50:51] op_sel_hi:[0,1,1]
	ds_write_b64 v10, v[40:41] offset:50688
	v_xor_b32_e32 v40, 0x80000000, v47
	v_mov_b32_e32 v41, v47
	v_pk_mul_f32 v[40:41], v[16:17], v[40:41] op_sel:[1,0] op_sel_hi:[0,1]
	v_pk_fma_f32 v[40:41], v[16:17], v[46:47], v[40:41] op_sel_hi:[1,0,1]
	v_xor_b32_e32 v46, 0x80000000, v69
	v_mov_b32_e32 v47, v69
	v_pk_mul_f32 v[46:47], v[46:47], v[40:41] op_sel:[0,1] op_sel_hi:[1,0]
	s_nop 0
	v_pk_fma_f32 v[46:47], v[68:69], v[40:41], v[46:47] op_sel_hi:[0,1,1]
	ds_write_b64 v10, v[46:47] offset:54912
	v_xor_b32_e32 v46, 0x80000000, v41
	v_mov_b32_e32 v47, v41
	v_pk_mul_f32 v[46:47], v[16:17], v[46:47] op_sel:[1,0] op_sel_hi:[0,1]
	v_pk_fma_f32 v[40:41], v[16:17], v[40:41], v[46:47] op_sel_hi:[1,0,1]
	v_xor_b32_e32 v46, 0x80000000, v45
	v_mov_b32_e32 v47, v45
	v_pk_mul_f32 v[46:47], v[46:47], v[40:41] op_sel:[0,1] op_sel_hi:[1,0]
	s_nop 0
	v_pk_fma_f32 v[44:45], v[44:45], v[40:41], v[46:47] op_sel_hi:[0,1,1]
	ds_write_b64 v10, v[44:45] offset:59136
	v_xor_b32_e32 v44, 0x80000000, v41
	v_mov_b32_e32 v45, v41
	v_pk_mul_f32 v[44:45], v[16:17], v[44:45] op_sel:[1,0] op_sel_hi:[0,1]
	v_pk_fma_f32 v[40:41], v[16:17], v[40:41], v[44:45] op_sel_hi:[1,0,1]
	v_xor_b32_e32 v44, 0x80000000, v63
	v_mov_b32_e32 v45, v63
	v_pk_mul_f32 v[44:45], v[44:45], v[40:41] op_sel:[0,1] op_sel_hi:[1,0]
	s_nop 0
	v_pk_fma_f32 v[44:45], v[62:63], v[40:41], v[44:45] op_sel_hi:[0,1,1]
	ds_write_b64 v10, v[44:45] offset:63360
	v_xor_b32_e32 v44, 0x80000000, v41
	v_mov_b32_e32 v45, v41
	v_pk_mul_f32 v[44:45], v[16:17], v[44:45] op_sel:[1,0] op_sel_hi:[0,1]
	v_pk_fma_f32 v[40:41], v[16:17], v[40:41], v[44:45] op_sel_hi:[1,0,1]
	v_xor_b32_e32 v44, 0x80000000, v31
	v_mov_b32_e32 v45, v31
	v_pk_mul_f32 v[44:45], v[44:45], v[40:41] op_sel:[0,1] op_sel_hi:[1,0]
	v_add_u32_e32 v13, 0x10800, v10
	v_pk_fma_f32 v[30:31], v[30:31], v[40:41], v[44:45] op_sel_hi:[0,1,1]
	ds_write_b64 v13, v[30:31]
	v_xor_b32_e32 v30, 0x80000000, v41
	v_mov_b32_e32 v31, v41
	v_pk_mul_f32 v[30:31], v[16:17], v[30:31] op_sel:[1,0] op_sel_hi:[0,1]
	v_pk_fma_f32 v[30:31], v[16:17], v[40:41], v[30:31] op_sel_hi:[1,0,1]
	v_xor_b32_e32 v40, 0x80000000, v55
	v_mov_b32_e32 v41, v55
	v_pk_mul_f32 v[40:41], v[40:41], v[30:31] op_sel:[0,1] op_sel_hi:[1,0]
	v_add_u32_e32 v13, 0x11880, v10
	v_pk_fma_f32 v[40:41], v[54:55], v[30:31], v[40:41] op_sel_hi:[0,1,1]
	ds_write_b64 v13, v[40:41]
	v_xor_b32_e32 v40, 0x80000000, v31
	v_mov_b32_e32 v41, v31
	v_pk_mul_f32 v[40:41], v[16:17], v[40:41] op_sel:[1,0] op_sel_hi:[0,1]
	v_pk_fma_f32 v[30:31], v[16:17], v[30:31], v[40:41] op_sel_hi:[1,0,1]
	v_xor_b32_e32 v40, 0x80000000, v35
	v_mov_b32_e32 v41, v35
	v_pk_mul_f32 v[40:41], v[40:41], v[30:31] op_sel:[0,1] op_sel_hi:[1,0]
	v_add_u32_e32 v13, 0x12900, v10
	v_pk_fma_f32 v[34:35], v[34:35], v[30:31], v[40:41] op_sel_hi:[0,1,1]
	ds_write_b64 v13, v[34:35]
	v_xor_b32_e32 v34, 0x80000000, v31
	v_mov_b32_e32 v35, v31
	v_pk_mul_f32 v[34:35], v[16:17], v[34:35] op_sel:[1,0] op_sel_hi:[0,1]
	v_pk_fma_f32 v[30:31], v[16:17], v[30:31], v[34:35] op_sel_hi:[1,0,1]
	v_xor_b32_e32 v34, 0x80000000, v67
	v_mov_b32_e32 v35, v67
	v_pk_mul_f32 v[34:35], v[34:35], v[30:31] op_sel:[0,1] op_sel_hi:[1,0]
	v_add_u32_e32 v13, 0x13980, v10
	v_pk_fma_f32 v[34:35], v[66:67], v[30:31], v[34:35] op_sel_hi:[0,1,1]
	ds_write_b64 v13, v[34:35]
	v_xor_b32_e32 v34, 0x80000000, v31
	v_mov_b32_e32 v35, v31
	v_pk_mul_f32 v[34:35], v[16:17], v[34:35] op_sel:[1,0] op_sel_hi:[0,1]
	v_pk_fma_f32 v[30:31], v[16:17], v[30:31], v[34:35] op_sel_hi:[1,0,1]
	v_xor_b32_e32 v34, 0x80000000, v27
	v_mov_b32_e32 v35, v27
	v_pk_mul_f32 v[34:35], v[34:35], v[30:31] op_sel:[0,1] op_sel_hi:[1,0]
	v_add_u32_e32 v13, 0x14a00, v10
	v_pk_fma_f32 v[26:27], v[26:27], v[30:31], v[34:35] op_sel_hi:[0,1,1]
	ds_write_b64 v13, v[26:27]
	v_xor_b32_e32 v26, 0x80000000, v31
	v_mov_b32_e32 v27, v31
	v_pk_mul_f32 v[26:27], v[16:17], v[26:27] op_sel:[1,0] op_sel_hi:[0,1]
	v_pk_fma_f32 v[26:27], v[16:17], v[30:31], v[26:27] op_sel_hi:[1,0,1]
	v_xor_b32_e32 v30, 0x80000000, v49
	v_mov_b32_e32 v31, v49
	v_pk_mul_f32 v[30:31], v[30:31], v[26:27] op_sel:[0,1] op_sel_hi:[1,0]
	v_add_u32_e32 v13, 0x15a80, v10
	v_pk_fma_f32 v[30:31], v[48:49], v[26:27], v[30:31] op_sel_hi:[0,1,1]
	ds_write_b64 v13, v[30:31]
	v_xor_b32_e32 v30, 0x80000000, v27
	v_mov_b32_e32 v31, v27
	v_pk_mul_f32 v[30:31], v[16:17], v[30:31] op_sel:[1,0] op_sel_hi:[0,1]
	v_pk_fma_f32 v[26:27], v[16:17], v[26:27], v[30:31] op_sel_hi:[1,0,1]
	v_xor_b32_e32 v30, 0x80000000, v29
	v_mov_b32_e32 v31, v29
	v_pk_mul_f32 v[30:31], v[30:31], v[26:27] op_sel:[0,1] op_sel_hi:[1,0]
	v_add_u32_e32 v13, 0x16b00, v10
	v_pk_fma_f32 v[28:29], v[28:29], v[26:27], v[30:31] op_sel_hi:[0,1,1]
	ds_write_b64 v13, v[28:29]
	v_xor_b32_e32 v28, 0x80000000, v27
	v_mov_b32_e32 v29, v27
	v_pk_mul_f32 v[28:29], v[16:17], v[28:29] op_sel:[1,0] op_sel_hi:[0,1]
	v_pk_fma_f32 v[26:27], v[16:17], v[26:27], v[28:29] op_sel_hi:[1,0,1]
	v_xor_b32_e32 v28, 0x80000000, v53
	v_mov_b32_e32 v29, v53
	v_pk_mul_f32 v[28:29], v[28:29], v[26:27] op_sel:[0,1] op_sel_hi:[1,0]
	v_add_u32_e32 v13, 0x17b80, v10
	v_pk_fma_f32 v[28:29], v[52:53], v[26:27], v[28:29] op_sel_hi:[0,1,1]
	ds_write_b64 v13, v[28:29]
	v_xor_b32_e32 v28, 0x80000000, v27
	v_mov_b32_e32 v29, v27
	v_pk_mul_f32 v[28:29], v[16:17], v[28:29] op_sel:[1,0] op_sel_hi:[0,1]
	v_pk_fma_f32 v[26:27], v[16:17], v[26:27], v[28:29] op_sel_hi:[1,0,1]
	v_xor_b32_e32 v28, 0x80000000, v23
	v_mov_b32_e32 v29, v23
	v_pk_mul_f32 v[28:29], v[28:29], v[26:27] op_sel:[0,1] op_sel_hi:[1,0]
	v_add_u32_e32 v13, 0x18c00, v10
	v_pk_fma_f32 v[22:23], v[22:23], v[26:27], v[28:29] op_sel_hi:[0,1,1]
	ds_write_b64 v13, v[22:23]
	v_xor_b32_e32 v22, 0x80000000, v27
	v_mov_b32_e32 v23, v27
	v_pk_mul_f32 v[22:23], v[16:17], v[22:23] op_sel:[1,0] op_sel_hi:[0,1]
	v_pk_fma_f32 v[22:23], v[16:17], v[26:27], v[22:23] op_sel_hi:[1,0,1]
	v_xor_b32_e32 v26, 0x80000000, v39
	v_mov_b32_e32 v27, v39
	v_pk_mul_f32 v[26:27], v[26:27], v[22:23] op_sel:[0,1] op_sel_hi:[1,0]
	v_add_u32_e32 v13, 0x19c80, v10
	v_pk_fma_f32 v[26:27], v[38:39], v[22:23], v[26:27] op_sel_hi:[0,1,1]
	ds_write_b64 v13, v[26:27]
	v_xor_b32_e32 v26, 0x80000000, v23
	v_mov_b32_e32 v27, v23
	v_pk_mul_f32 v[26:27], v[16:17], v[26:27] op_sel:[1,0] op_sel_hi:[0,1]
	v_pk_fma_f32 v[22:23], v[16:17], v[22:23], v[26:27] op_sel_hi:[1,0,1]
	v_xor_b32_e32 v26, 0x80000000, v25
	v_mov_b32_e32 v27, v25
	v_pk_mul_f32 v[26:27], v[26:27], v[22:23] op_sel:[0,1] op_sel_hi:[1,0]
	v_add_u32_e32 v13, 0x1ad00, v10
	v_pk_fma_f32 v[24:25], v[24:25], v[22:23], v[26:27] op_sel_hi:[0,1,1]
	ds_write_b64 v13, v[24:25]
	v_xor_b32_e32 v24, 0x80000000, v23
	v_mov_b32_e32 v25, v23
	v_pk_mul_f32 v[24:25], v[16:17], v[24:25] op_sel:[1,0] op_sel_hi:[0,1]
	v_pk_fma_f32 v[22:23], v[16:17], v[22:23], v[24:25] op_sel_hi:[1,0,1]
	v_xor_b32_e32 v24, 0x80000000, v43
	v_mov_b32_e32 v25, v43
	v_pk_mul_f32 v[24:25], v[24:25], v[22:23] op_sel:[0,1] op_sel_hi:[1,0]
	v_add_u32_e32 v13, 0x1bd80, v10
	v_pk_fma_f32 v[24:25], v[42:43], v[22:23], v[24:25] op_sel_hi:[0,1,1]
	ds_write_b64 v13, v[24:25]
	v_xor_b32_e32 v24, 0x80000000, v23
	v_mov_b32_e32 v25, v23
	v_pk_mul_f32 v[24:25], v[16:17], v[24:25] op_sel:[1,0] op_sel_hi:[0,1]
	v_pk_fma_f32 v[22:23], v[16:17], v[22:23], v[24:25] op_sel_hi:[1,0,1]
	v_xor_b32_e32 v24, 0x80000000, v19
	v_mov_b32_e32 v25, v19
	v_pk_mul_f32 v[24:25], v[24:25], v[22:23] op_sel:[0,1] op_sel_hi:[1,0]
	v_add_u32_e32 v13, 0x1ce00, v10
	v_pk_fma_f32 v[18:19], v[18:19], v[22:23], v[24:25] op_sel_hi:[0,1,1]
	ds_write_b64 v13, v[18:19]
	v_xor_b32_e32 v18, 0x80000000, v23
	v_mov_b32_e32 v19, v23
	v_pk_mul_f32 v[18:19], v[16:17], v[18:19] op_sel:[1,0] op_sel_hi:[0,1]
	v_pk_fma_f32 v[18:19], v[16:17], v[22:23], v[18:19] op_sel_hi:[1,0,1]
	v_xor_b32_e32 v22, 0x80000000, v33
	v_mov_b32_e32 v23, v33
	v_pk_mul_f32 v[22:23], v[22:23], v[18:19] op_sel:[0,1] op_sel_hi:[1,0]
	v_add_u32_e32 v13, 0x1de80, v10
	v_pk_fma_f32 v[22:23], v[32:33], v[18:19], v[22:23] op_sel_hi:[0,1,1]
	ds_write_b64 v13, v[22:23]
	v_xor_b32_e32 v22, 0x80000000, v19
	v_mov_b32_e32 v23, v19
	v_pk_mul_f32 v[22:23], v[16:17], v[22:23] op_sel:[1,0] op_sel_hi:[0,1]
	v_pk_fma_f32 v[18:19], v[16:17], v[18:19], v[22:23] op_sel_hi:[1,0,1]
	v_xor_b32_e32 v22, 0x80000000, v21
	v_mov_b32_e32 v23, v21
	v_pk_mul_f32 v[22:23], v[22:23], v[18:19] op_sel:[0,1] op_sel_hi:[1,0]
	v_add_u32_e32 v13, 0x1ef00, v10
	v_pk_fma_f32 v[20:21], v[20:21], v[18:19], v[22:23] op_sel_hi:[0,1,1]
	ds_write_b64 v13, v[20:21]
	v_xor_b32_e32 v20, 0x80000000, v19
	v_mov_b32_e32 v21, v19
	v_pk_mul_f32 v[20:21], v[16:17], v[20:21] op_sel:[1,0] op_sel_hi:[0,1]
	v_pk_fma_f32 v[16:17], v[16:17], v[18:19], v[20:21] op_sel_hi:[1,0,1]
	v_xor_b32_e32 v18, 0x80000000, v37
	v_mov_b32_e32 v19, v37
	v_pk_mul_f32 v[18:19], v[18:19], v[16:17] op_sel:[0,1] op_sel_hi:[1,0]
	v_add_u32_e32 v10, 0x1ff80, v10
	v_pk_fma_f32 v[16:17], v[36:37], v[16:17], v[18:19] op_sel_hi:[0,1,1]
	ds_write_b64 v10, v[16:17]
	v_mov_b32_e32 v10, v176
	v_mov_b32_e32 v13, v173
	s_waitcnt lgkmcnt(0)
	s_barrier
	v_mov_b32_e32 v16, v182
	v_add_u32_e32 v15, v13, v10
	v_lshl_add_u32 v75, v15, 3, 0
	v_xad_u32 v15, v13, 1, v10
	v_lshl_add_u32 v74, v15, 3, 0
	v_xad_u32 v15, v13, 2, v10
	v_lshl_add_u32 v73, v15, 3, 0
	v_xad_u32 v15, v13, 3, v10
	v_lshl_add_u32 v72, v15, 3, 0
	v_xad_u32 v15, v13, 4, v10
	v_lshl_add_u32 v71, v15, 3, 0
	v_xad_u32 v15, v13, 5, v10
	v_lshl_add_u32 v70, v15, 3, 0
	v_xad_u32 v15, v13, 6, v10
	v_lshl_add_u32 v69, v15, 3, 0
	v_xad_u32 v15, v13, 7, v10
	v_lshl_add_u32 v68, v15, 3, 0
	v_xad_u32 v15, v13, 8, v10
	v_lshl_add_u32 v15, v15, 3, 0
	v_add_u32_e32 v67, 0x800, v15
	v_xad_u32 v15, v13, 9, v10
	v_lshl_add_u32 v15, v15, 3, 0
	v_add_u32_e32 v66, 0x800, v15
	v_xad_u32 v15, v13, 10, v10
	v_lshl_add_u32 v15, v15, 3, 0
	v_add_u32_e32 v65, 0x800, v15
	v_xad_u32 v15, v13, 11, v10
	v_lshl_add_u32 v15, v15, 3, 0
	v_add_u32_e32 v64, 0x800, v15
	v_xad_u32 v15, v13, 12, v10
	v_mov_b32_e32 v17, v183
	v_lshl_add_u32 v15, v15, 3, 0
	ds_read2_b64 v[18:21], v75 offset1:16
	ds_read2_b64 v[40:43], v67 offset1:16
	v_add_u32_e32 v63, 0x800, v15
	v_xad_u32 v15, v13, 13, v10
	v_lshl_add_u32 v15, v15, 3, 0
	v_add_u32_e32 v62, 0x800, v15
	v_xad_u32 v15, v13, 14, v10
	v_xad_u32 v10, v13, 15, v10
	ds_read2_b64 v[22:25], v74 offset0:32 offset1:48
	ds_read2_b64 v[48:51], v66 offset0:32 offset1:48
	v_lshl_add_u32 v15, v15, 3, 0
	v_lshl_add_u32 v10, v10, 3, 0
	v_add_u32_e32 v15, 0x800, v15
	v_add_u32_e32 v13, 0x800, v10
	v_mov_b32_e32 v10, v164
	ds_read2_b64 v[26:29], v73 offset0:64 offset1:80
	ds_read2_b64 v[58:61], v72 offset0:96 offset1:112
	ds_read2_b64 v[76:79], v71 offset0:128 offset1:144
	ds_read2_b64 v[80:83], v70 offset0:160 offset1:176
	ds_read2_b64 v[84:87], v69 offset0:192 offset1:208
	ds_read2_b64 v[88:91], v68 offset0:224 offset1:240
	ds_read2_b64 v[54:57], v65 offset0:64 offset1:80
	ds_read2_b64 v[92:95], v64 offset0:96 offset1:112
	ds_read2_b64 v[96:99], v63 offset0:128 offset1:144
	ds_read2_b64 v[100:103], v62 offset0:160 offset1:176
	ds_read2_b64 v[104:107], v15 offset0:192 offset1:208
	ds_read2_b64 v[108:111], v13 offset0:224 offset1:240
	s_waitcnt lgkmcnt(14)
	v_pk_add_f32 v[112:113], v[18:19], v[40:41]
	v_pk_add_f32 v[40:41], v[18:19], v[40:41] neg_lo:[0,1] neg_hi:[0,1]
	v_pk_add_f32 v[18:19], v[20:21], v[42:43]
	v_pk_add_f32 v[20:21], v[20:21], v[42:43] neg_lo:[0,1] neg_hi:[0,1]
	v_mov_b32_e32 v30, v165
	v_mov_b32_e32 v32, v166
	v_mov_b32_e32 v34, v167
	v_mov_b32_e32 v10, v168
	v_mov_b32_e32 v38, v169
	v_mov_b32_e32 v36, v170
	v_mov_b32_e32 v46, v171
	v_xor_b32_e32 v42, 0x80000000, v21
	v_mov_b32_e32 v43, v20
	v_mov_b32_e32 v31, v172
	v_pk_mul_f32 v[42:43], v[42:43], v[46:47] op_sel_hi:[1,0] neg_lo:[0,1] neg_hi:[0,1]
	s_nop 0
	v_pk_fma_f32 v[44:45], v[20:21], v[30:31], v[42:43] op_sel_hi:[1,0,1]
	s_waitcnt lgkmcnt(12)
	v_pk_add_f32 v[20:21], v[22:23], v[48:49]
	v_pk_add_f32 v[22:23], v[22:23], v[48:49] neg_lo:[0,1] neg_hi:[0,1]
	s_nop 0
	v_xor_b32_e32 v42, 0x80000000, v23
	v_mov_b32_e32 v43, v22
	v_pk_mul_f32 v[42:43], v[42:43], v[36:37] op_sel_hi:[1,0] neg_lo:[0,1] neg_hi:[0,1]
	s_nop 0
	v_pk_fma_f32 v[48:49], v[22:23], v[32:33], v[42:43] op_sel_hi:[1,0,1]
	v_pk_add_f32 v[22:23], v[24:25], v[50:51]
	v_pk_add_f32 v[24:25], v[24:25], v[50:51] neg_lo:[0,1] neg_hi:[0,1]
	s_nop 0
	v_xor_b32_e32 v42, 0x80000000, v25
	v_mov_b32_e32 v43, v24
	v_pk_mul_f32 v[42:43], v[42:43], v[38:39] op_sel_hi:[1,0] neg_lo:[0,1] neg_hi:[0,1]
	s_nop 0
	v_pk_fma_f32 v[52:53], v[24:25], v[34:35], v[42:43] op_sel_hi:[1,0,1]
	s_waitcnt lgkmcnt(5)
	v_pk_add_f32 v[24:25], v[26:27], v[54:55]
	v_pk_add_f32 v[26:27], v[26:27], v[54:55] neg_lo:[0,1] neg_hi:[0,1]
	s_nop 0
	v_xor_b32_e32 v42, 0x80000000, v27
	v_mov_b32_e32 v43, v26
	v_pk_mul_f32 v[42:43], v[42:43], v[10:11] op_sel_hi:[1,0] neg_lo:[0,1] neg_hi:[0,1]
	s_nop 0
	v_pk_fma_f32 v[54:55], v[26:27], v[10:11], v[42:43] op_sel_hi:[1,0,1]
	v_pk_add_f32 v[26:27], v[28:29], v[56:57]
	v_pk_add_f32 v[28:29], v[28:29], v[56:57] neg_lo:[0,1] neg_hi:[0,1]
	s_nop 0
	v_pk_mul_f32 v[42:43], v[28:29], v[38:39] op_sel_hi:[1,0]
	v_xor_b32_e32 v50, 0x80000000, v29
	v_mov_b32_e32 v51, v28
	v_pk_fma_f32 v[56:57], v[50:51], v[34:35], v[42:43] op_sel_hi:[1,0,1] neg_lo:[0,1,0] neg_hi:[0,1,0]
	s_waitcnt lgkmcnt(4)
	v_pk_add_f32 v[42:43], v[58:59], v[92:93] neg_lo:[0,1] neg_hi:[0,1]
	v_pk_add_f32 v[28:29], v[58:59], v[92:93]
	v_pk_mul_f32 v[50:51], v[42:43], v[36:37] op_sel_hi:[1,0]
	v_xor_b32_e32 v58, 0x80000000, v43
	v_mov_b32_e32 v59, v42
	v_pk_fma_f32 v[58:59], v[58:59], v[32:33], v[50:51] op_sel_hi:[1,0,1] neg_lo:[0,1,0] neg_hi:[0,1,0]
	v_pk_add_f32 v[50:51], v[60:61], v[94:95] neg_lo:[0,1] neg_hi:[0,1]
	v_pk_add_f32 v[42:43], v[60:61], v[94:95]
	v_pk_mul_f32 v[60:61], v[50:51], v[46:47] op_sel_hi:[1,0]
	v_xor_b32_e32 v92, 0x80000000, v51
	v_mov_b32_e32 v93, v50
	s_waitcnt lgkmcnt(3)
	v_pk_add_f32 v[50:51], v[76:77], v[96:97]
	v_pk_add_f32 v[76:77], v[76:77], v[96:97] neg_lo:[0,1] neg_hi:[0,1]
	v_pk_fma_f32 v[60:61], v[92:93], v[30:31], v[60:61] op_sel_hi:[1,0,1] neg_lo:[0,1,0] neg_hi:[0,1,0]
	v_xor_b32_e32 v93, 0x80000000, v76
	v_mov_b32_e32 v92, v77
	v_pk_add_f32 v[76:77], v[78:79], v[98:99]
	v_pk_add_f32 v[78:79], v[78:79], v[98:99] neg_lo:[0,1] neg_hi:[0,1]
	s_nop 0
	v_pk_mul_f32 v[94:95], v[78:79], v[46:47] op_sel_hi:[1,0] neg_lo:[0,1] neg_hi:[0,1]
	v_xor_b32_e32 v96, 0x80000000, v79
	v_mov_b32_e32 v97, v78
	v_pk_fma_f32 v[78:79], v[96:97], v[30:31], v[94:95] op_sel_hi:[1,0,1] neg_lo:[0,1,0] neg_hi:[0,1,0]
	s_waitcnt lgkmcnt(2)
	v_pk_add_f32 v[94:95], v[80:81], v[100:101]
	v_pk_add_f32 v[80:81], v[80:81], v[100:101] neg_lo:[0,1] neg_hi:[0,1]
	s_nop 0
	v_pk_mul_f32 v[96:97], v[80:81], v[36:37] op_sel_hi:[1,0] neg_lo:[0,1] neg_hi:[0,1]
	v_xor_b32_e32 v98, 0x80000000, v81
	v_mov_b32_e32 v99, v80
	v_pk_fma_f32 v[80:81], v[98:99], v[32:33], v[96:97] op_sel_hi:[1,0,1] neg_lo:[0,1,0] neg_hi:[0,1,0]
	v_pk_add_f32 v[96:97], v[82:83], v[102:103]
	v_pk_add_f32 v[82:83], v[82:83], v[102:103] neg_lo:[0,1] neg_hi:[0,1]
	s_nop 0
	v_pk_mul_f32 v[98:99], v[82:83], v[38:39] op_sel_hi:[1,0] neg_lo:[0,1] neg_hi:[0,1]
	v_xor_b32_e32 v100, 0x80000000, v83
	v_mov_b32_e32 v101, v82
	v_pk_fma_f32 v[82:83], v[100:101], v[34:35], v[98:99] op_sel_hi:[1,0,1] neg_lo:[0,1,0] neg_hi:[0,1,0]
	s_waitcnt lgkmcnt(1)
	v_pk_add_f32 v[98:99], v[84:85], v[104:105]
	v_pk_add_f32 v[84:85], v[84:85], v[104:105] neg_lo:[0,1] neg_hi:[0,1]
	s_nop 0
	v_xor_b32_e32 v100, 0x80000000, v85
	v_mov_b32_e32 v101, v84
	v_pk_mul_f32 v[100:101], v[100:101], v[10:11] op_sel_hi:[1,0] neg_lo:[0,1] neg_hi:[0,1]
	s_nop 0
	v_pk_fma_f32 v[84:85], v[84:85], v[10:11], v[100:101] op_sel_hi:[1,0,1] neg_lo:[0,1,0] neg_hi:[0,1,0]
	v_pk_add_f32 v[100:101], v[86:87], v[106:107]
	v_pk_add_f32 v[86:87], v[86:87], v[106:107] neg_lo:[0,1] neg_hi:[0,1]
	s_nop 0
	v_xor_b32_e32 v102, 0x80000000, v87
	v_mov_b32_e32 v103, v86
	v_pk_mul_f32 v[38:39], v[102:103], v[38:39] op_sel_hi:[1,0] neg_lo:[0,1] neg_hi:[0,1]
	s_nop 0
	v_pk_fma_f32 v[86:87], v[86:87], v[34:35], v[38:39] op_sel_hi:[1,0,1] neg_lo:[0,1,0] neg_hi:[0,1,0]
	s_waitcnt lgkmcnt(0)
	v_pk_add_f32 v[38:39], v[88:89], v[108:109] neg_lo:[0,1] neg_hi:[0,1]
	v_pk_add_f32 v[34:35], v[88:89], v[108:109]
	v_xor_b32_e32 v88, 0x80000000, v39
	v_mov_b32_e32 v89, v38
	v_pk_mul_f32 v[88:89], v[88:89], v[36:37] op_sel_hi:[1,0] neg_lo:[0,1] neg_hi:[0,1]
	s_nop 0
	v_pk_fma_f32 v[88:89], v[38:39], v[32:33], v[88:89] op_sel_hi:[1,0,1] neg_lo:[0,1,0] neg_hi:[0,1,0]
	v_pk_add_f32 v[38:39], v[90:91], v[110:111]
	v_pk_add_f32 v[90:91], v[90:91], v[110:111] neg_lo:[0,1] neg_hi:[0,1]
	s_nop 0
	v_xor_b32_e32 v102, 0x80000000, v91
	v_mov_b32_e32 v103, v90
	v_pk_mul_f32 v[46:47], v[102:103], v[46:47] op_sel_hi:[1,0] neg_lo:[0,1] neg_hi:[0,1]
	s_nop 0
	v_pk_fma_f32 v[90:91], v[90:91], v[30:31], v[46:47] op_sel_hi:[1,0,1] neg_lo:[0,1,0] neg_hi:[0,1,0]
	v_pk_add_f32 v[46:47], v[18:19], v[76:77]
	v_pk_add_f32 v[18:19], v[18:19], v[76:77] neg_lo:[0,1] neg_hi:[0,1]
	v_pk_add_f32 v[30:31], v[112:113], v[50:51]
	v_xor_b32_e32 v76, 0x80000000, v19
	v_mov_b32_e32 v77, v18
	v_pk_mul_f32 v[76:77], v[76:77], v[36:37] op_sel_hi:[1,0] neg_lo:[0,1] neg_hi:[0,1]
	v_pk_add_f32 v[50:51], v[112:113], v[50:51] neg_lo:[0,1] neg_hi:[0,1]
	v_pk_fma_f32 v[76:77], v[18:19], v[32:33], v[76:77] op_sel_hi:[1,0,1]
	v_pk_add_f32 v[18:19], v[20:21], v[94:95]
	v_pk_add_f32 v[20:21], v[20:21], v[94:95] neg_lo:[0,1] neg_hi:[0,1]
	s_nop 0
	v_xor_b32_e32 v94, 0x80000000, v21
	v_mov_b32_e32 v95, v20
	v_pk_mul_f32 v[94:95], v[94:95], v[10:11] op_sel_hi:[1,0] neg_lo:[0,1] neg_hi:[0,1]
	s_nop 0
	v_pk_fma_f32 v[20:21], v[20:21], v[10:11], v[94:95] op_sel_hi:[1,0,1]
	v_pk_add_f32 v[94:95], v[22:23], v[96:97]
	v_pk_add_f32 v[22:23], v[22:23], v[96:97] neg_lo:[0,1] neg_hi:[0,1]
	s_nop 0
	v_pk_mul_f32 v[96:97], v[22:23], v[36:37] op_sel_hi:[1,0]
	v_xor_b32_e32 v102, 0x80000000, v23
	v_mov_b32_e32 v103, v22
	v_pk_add_f32 v[22:23], v[24:25], v[98:99]
	v_pk_add_f32 v[24:25], v[24:25], v[98:99] neg_lo:[0,1] neg_hi:[0,1]
	v_pk_fma_f32 v[96:97], v[102:103], v[32:33], v[96:97] op_sel_hi:[1,0,1] neg_lo:[0,1,0] neg_hi:[0,1,0]
	v_xor_b32_e32 v99, 0x80000000, v24
	v_mov_b32_e32 v98, v25
	v_pk_add_f32 v[24:25], v[26:27], v[100:101]
	v_pk_add_f32 v[26:27], v[26:27], v[100:101] neg_lo:[0,1] neg_hi:[0,1]
	s_nop 0
	v_pk_mul_f32 v[100:101], v[26:27], v[36:37] op_sel_hi:[1,0] neg_lo:[0,1] neg_hi:[0,1]
	v_xor_b32_e32 v102, 0x80000000, v27
	v_mov_b32_e32 v103, v26
	v_pk_add_f32 v[26:27], v[28:29], v[34:35]
	v_pk_add_f32 v[28:29], v[28:29], v[34:35] neg_lo:[0,1] neg_hi:[0,1]
	v_pk_fma_f32 v[100:101], v[102:103], v[32:33], v[100:101] op_sel_hi:[1,0,1] neg_lo:[0,1,0] neg_hi:[0,1,0]
	v_xor_b32_e32 v34, 0x80000000, v29
	v_mov_b32_e32 v35, v28
	v_pk_mul_f32 v[34:35], v[34:35], v[10:11] op_sel_hi:[1,0] neg_lo:[0,1] neg_hi:[0,1]
	v_pk_add_f32 v[102:103], v[30:31], v[22:23] neg_lo:[0,1] neg_hi:[0,1]
	v_pk_fma_f32 v[28:29], v[28:29], v[10:11], v[34:35] op_sel_hi:[1,0,1] neg_lo:[0,1,0] neg_hi:[0,1,0]
	v_pk_add_f32 v[34:35], v[42:43], v[38:39]
	v_pk_add_f32 v[38:39], v[42:43], v[38:39] neg_lo:[0,1] neg_hi:[0,1]
	s_nop 0
	v_xor_b32_e32 v42, 0x80000000, v39
	v_mov_b32_e32 v43, v38
	v_pk_mul_f32 v[42:43], v[42:43], v[36:37] op_sel_hi:[1,0] neg_lo:[0,1] neg_hi:[0,1]
	s_nop 0
	v_pk_fma_f32 v[42:43], v[38:39], v[32:33], v[42:43] op_sel_hi:[1,0,1] neg_lo:[0,1,0] neg_hi:[0,1,0]
	v_pk_add_f32 v[38:39], v[30:31], v[22:23]
	v_pk_add_f32 v[22:23], v[46:47], v[24:25]
	v_pk_add_f32 v[24:25], v[46:47], v[24:25] neg_lo:[0,1] neg_hi:[0,1]
	s_nop 0
	v_xor_b32_e32 v30, 0x80000000, v25
	v_mov_b32_e32 v31, v24
	v_pk_mul_f32 v[30:31], v[30:31], v[10:11] op_sel_hi:[1,0] neg_lo:[0,1] neg_hi:[0,1]
	s_nop 0
	v_pk_fma_f32 v[24:25], v[24:25], v[10:11], v[30:31] op_sel_hi:[1,0,1]
	v_pk_add_f32 v[30:31], v[18:19], v[26:27]
	v_pk_add_f32 v[18:19], v[18:19], v[26:27] neg_lo:[0,1] neg_hi:[0,1]
	s_nop 0
	v_xor_b32_e32 v27, 0x80000000, v18
	v_mov_b32_e32 v26, v19
	v_pk_add_f32 v[18:19], v[94:95], v[34:35]
	v_pk_add_f32 v[34:35], v[94:95], v[34:35] neg_lo:[0,1] neg_hi:[0,1]
	s_nop 0
	v_xor_b32_e32 v46, 0x80000000, v35
	v_mov_b32_e32 v47, v34
	v_pk_mul_f32 v[46:47], v[46:47], v[10:11] op_sel_hi:[1,0] neg_lo:[0,1] neg_hi:[0,1]
	s_nop 0
	v_pk_fma_f32 v[34:35], v[34:35], v[10:11], v[46:47] op_sel_hi:[1,0,1] neg_lo:[0,1,0] neg_hi:[0,1,0]
	v_pk_add_f32 v[46:47], v[38:39], v[30:31]
	v_pk_add_f32 v[38:39], v[38:39], v[30:31] neg_lo:[0,1] neg_hi:[0,1]
	v_pk_add_f32 v[30:31], v[22:23], v[18:19]
	v_pk_add_f32 v[18:19], v[22:23], v[18:19] neg_lo:[0,1] neg_hi:[0,1]
	v_pk_add_f32 v[94:95], v[46:47], v[30:31]
	v_xor_b32_e32 v23, 0x80000000, v18
	v_mov_b32_e32 v22, v19
	v_pk_add_f32 v[18:19], v[102:103], v[26:27]
	v_pk_add_f32 v[102:103], v[102:103], v[26:27] neg_lo:[0,1] neg_hi:[0,1]
	v_pk_add_f32 v[26:27], v[24:25], v[34:35]
	v_pk_add_f32 v[24:25], v[24:25], v[34:35] neg_lo:[0,1] neg_hi:[0,1]
	v_pk_add_f32 v[30:31], v[46:47], v[30:31] neg_lo:[0,1] neg_hi:[0,1]
	v_xor_b32_e32 v35, 0x80000000, v24
	v_mov_b32_e32 v34, v25
	v_pk_add_f32 v[24:25], v[50:51], v[98:99]
	v_pk_add_f32 v[98:99], v[50:51], v[98:99] neg_lo:[0,1] neg_hi:[0,1]
	v_pk_add_f32 v[50:51], v[76:77], v[100:101] neg_lo:[0,1] neg_hi:[0,1]
	v_pk_add_f32 v[46:47], v[38:39], v[22:23]
	v_pk_add_f32 v[22:23], v[38:39], v[22:23] neg_lo:[0,1] neg_hi:[0,1]
	v_pk_add_f32 v[104:105], v[18:19], v[26:27]
	v_pk_add_f32 v[26:27], v[18:19], v[26:27] neg_lo:[0,1] neg_hi:[0,1]
	v_pk_add_f32 v[38:39], v[102:103], v[34:35]
	v_pk_add_f32 v[18:19], v[102:103], v[34:35] neg_lo:[0,1] neg_hi:[0,1]
	v_pk_add_f32 v[34:35], v[76:77], v[100:101]
	v_xor_b32_e32 v76, 0x80000000, v51
	v_mov_b32_e32 v77, v50
	v_pk_mul_f32 v[76:77], v[10:11], v[76:77] op_sel_hi:[0,1] neg_lo:[1,0] neg_hi:[1,0]
	v_pk_fma_f32 v[76:77], v[10:11], v[50:51], v[76:77] op_sel_hi:[0,1,1]
	v_pk_add_f32 v[50:51], v[20:21], v[28:29]
	v_pk_add_f32 v[20:21], v[20:21], v[28:29] neg_lo:[0,1] neg_hi:[0,1]
	s_nop 0
	v_xor_b32_e32 v29, 0x80000000, v20
	v_mov_b32_e32 v28, v21
	v_pk_add_f32 v[20:21], v[96:97], v[42:43]
	v_pk_add_f32 v[42:43], v[96:97], v[42:43] neg_lo:[0,1] neg_hi:[0,1]
	s_nop 0
	v_xor_b32_e32 v96, 0x80000000, v43
	v_mov_b32_e32 v97, v42
	v_pk_mul_f32 v[96:97], v[10:11], v[96:97] op_sel_hi:[0,1] neg_lo:[1,0] neg_hi:[1,0]
	v_pk_fma_f32 v[42:43], v[10:11], v[42:43], v[96:97] op_sel_hi:[0,1,1] neg_lo:[1,0,0] neg_hi:[1,0,0]
	v_pk_add_f32 v[96:97], v[24:25], v[50:51]
	v_pk_add_f32 v[24:25], v[24:25], v[50:51] neg_lo:[0,1] neg_hi:[0,1]
	v_pk_add_f32 v[50:51], v[34:35], v[20:21]
	v_pk_add_f32 v[20:21], v[34:35], v[20:21] neg_lo:[0,1] neg_hi:[0,1]
	v_pk_add_f32 v[102:103], v[96:97], v[50:51]
	v_xor_b32_e32 v101, 0x80000000, v20
	v_mov_b32_e32 v100, v21
	v_pk_add_f32 v[34:35], v[96:97], v[50:51] neg_lo:[0,1] neg_hi:[0,1]
	v_pk_add_f32 v[20:21], v[98:99], v[28:29]
	v_pk_add_f32 v[96:97], v[98:99], v[28:29] neg_lo:[0,1] neg_hi:[0,1]
	v_pk_add_f32 v[28:29], v[76:77], v[42:43]
	v_pk_add_f32 v[42:43], v[76:77], v[42:43] neg_lo:[0,1] neg_hi:[0,1]
	v_pk_add_f32 v[98:99], v[20:21], v[28:29]
	v_xor_b32_e32 v77, 0x80000000, v42
	v_mov_b32_e32 v76, v43
	v_pk_add_f32 v[28:29], v[20:21], v[28:29] neg_lo:[0,1] neg_hi:[0,1]
	v_pk_add_f32 v[42:43], v[96:97], v[76:77]
	v_pk_add_f32 v[20:21], v[96:97], v[76:77] neg_lo:[0,1] neg_hi:[0,1]
	v_pk_add_f32 v[76:77], v[40:41], v[92:93]
	v_pk_add_f32 v[92:93], v[40:41], v[92:93] neg_lo:[0,1] neg_hi:[0,1]
	v_pk_add_f32 v[40:41], v[44:45], v[78:79]
	v_pk_add_f32 v[44:45], v[44:45], v[78:79] neg_lo:[0,1] neg_hi:[0,1]
	v_pk_add_f32 v[50:51], v[24:25], v[100:101]
	v_xor_b32_e32 v78, 0x80000000, v45
	v_mov_b32_e32 v79, v44
	v_pk_mul_f32 v[78:79], v[36:37], v[78:79] op_sel_hi:[0,1] neg_lo:[1,0] neg_hi:[1,0]
	v_pk_fma_f32 v[44:45], v[32:33], v[44:45], v[78:79] op_sel_hi:[0,1,1]
	v_pk_add_f32 v[78:79], v[48:49], v[80:81]
	v_pk_add_f32 v[48:49], v[48:49], v[80:81] neg_lo:[0,1] neg_hi:[0,1]
	v_pk_add_f32 v[24:25], v[24:25], v[100:101] neg_lo:[0,1] neg_hi:[0,1]
	v_xor_b32_e32 v80, 0x80000000, v49
	v_mov_b32_e32 v81, v48
	v_pk_mul_f32 v[80:81], v[10:11], v[80:81] op_sel_hi:[0,1] neg_lo:[1,0] neg_hi:[1,0]
	v_pk_fma_f32 v[80:81], v[10:11], v[48:49], v[80:81] op_sel_hi:[0,1,1]
	v_pk_add_f32 v[48:49], v[52:53], v[82:83]
	v_pk_add_f32 v[52:53], v[52:53], v[82:83] neg_lo:[0,1] neg_hi:[0,1]
	s_nop 0
	v_xor_b32_e32 v82, 0x80000000, v53
	v_mov_b32_e32 v83, v52
	v_pk_mul_f32 v[82:83], v[32:33], v[82:83] op_sel_hi:[0,1] neg_lo:[1,0] neg_hi:[1,0]
	v_pk_fma_f32 v[52:53], v[36:37], v[52:53], v[82:83] op_sel_hi:[0,1,1]
	v_pk_add_f32 v[82:83], v[54:55], v[84:85]
	v_pk_add_f32 v[54:55], v[54:55], v[84:85] neg_lo:[0,1] neg_hi:[0,1]
	s_nop 0
	v_xor_b32_e32 v85, 0x80000000, v54
	v_mov_b32_e32 v84, v55
	v_pk_add_f32 v[54:55], v[56:57], v[86:87]
	v_pk_add_f32 v[56:57], v[56:57], v[86:87] neg_lo:[0,1] neg_hi:[0,1]
	s_nop 0
	v_xor_b32_e32 v86, 0x80000000, v57
	v_mov_b32_e32 v87, v56
	v_pk_mul_f32 v[86:87], v[32:33], v[86:87] op_sel_hi:[0,1] neg_lo:[1,0] neg_hi:[1,0]
	v_pk_fma_f32 v[56:57], v[36:37], v[56:57], v[86:87] op_sel_hi:[0,1,1] neg_lo:[1,0,0] neg_hi:[1,0,0]
	v_pk_add_f32 v[86:87], v[58:59], v[88:89]
	v_pk_add_f32 v[58:59], v[58:59], v[88:89] neg_lo:[0,1] neg_hi:[0,1]
	s_nop 0
	v_xor_b32_e32 v88, 0x80000000, v59
	v_mov_b32_e32 v89, v58
	v_pk_mul_f32 v[88:89], v[10:11], v[88:89] op_sel_hi:[0,1] neg_lo:[1,0] neg_hi:[1,0]
	v_pk_fma_f32 v[58:59], v[10:11], v[58:59], v[88:89] op_sel_hi:[0,1,1] neg_lo:[1,0,0] neg_hi:[1,0,0]
	v_pk_add_f32 v[88:89], v[60:61], v[90:91]
	v_pk_add_f32 v[60:61], v[60:61], v[90:91] neg_lo:[0,1] neg_hi:[0,1]
	s_nop 0
	v_xor_b32_e32 v90, 0x80000000, v61
	v_mov_b32_e32 v91, v60
	v_pk_mul_f32 v[36:37], v[36:37], v[90:91] op_sel_hi:[0,1] neg_lo:[1,0] neg_hi:[1,0]
	v_pk_fma_f32 v[36:37], v[32:33], v[60:61], v[36:37] op_sel_hi:[0,1,1] neg_lo:[1,0,0] neg_hi:[1,0,0]
	v_pk_add_f32 v[32:33], v[76:77], v[82:83]
	v_pk_add_f32 v[60:61], v[76:77], v[82:83] neg_lo:[0,1] neg_hi:[0,1]
	v_pk_add_f32 v[76:77], v[54:55], v[40:41]
	v_pk_add_f32 v[40:41], v[40:41], v[54:55] neg_lo:[0,1] neg_hi:[0,1]
	s_nop 0
	v_xor_b32_e32 v54, 0x80000000, v41
	v_mov_b32_e32 v55, v40
	v_pk_mul_f32 v[54:55], v[10:11], v[54:55] op_sel_hi:[0,1] neg_lo:[1,0] neg_hi:[1,0]
	v_pk_fma_f32 v[54:55], v[10:11], v[40:41], v[54:55] op_sel_hi:[0,1,1]
	v_pk_add_f32 v[40:41], v[78:79], v[86:87]
	v_pk_add_f32 v[78:79], v[78:79], v[86:87] neg_lo:[0,1] neg_hi:[0,1]
	s_nop 0
	v_xor_b32_e32 v83, 0x80000000, v78
	v_mov_b32_e32 v82, v79
	v_pk_add_f32 v[78:79], v[48:49], v[88:89]
	v_pk_add_f32 v[48:49], v[48:49], v[88:89] neg_lo:[0,1] neg_hi:[0,1]
	v_pk_add_f32 v[88:89], v[76:77], v[78:79]
	v_xor_b32_e32 v86, 0x80000000, v49
	v_mov_b32_e32 v87, v48
	v_pk_mul_f32 v[86:87], v[10:11], v[86:87] op_sel_hi:[0,1] neg_lo:[1,0] neg_hi:[1,0]
	v_pk_fma_f32 v[48:49], v[10:11], v[48:49], v[86:87] op_sel_hi:[0,1,1] neg_lo:[1,0,0] neg_hi:[1,0,0]
	v_pk_add_f32 v[86:87], v[32:33], v[40:41]
	v_pk_add_f32 v[32:33], v[32:33], v[40:41] neg_lo:[0,1] neg_hi:[0,1]
	v_pk_add_f32 v[40:41], v[76:77], v[78:79] neg_lo:[0,1] neg_hi:[0,1]
	v_pk_add_f32 v[78:79], v[86:87], v[88:89] neg_lo:[0,1] neg_hi:[0,1]
	v_xor_b32_e32 v77, 0x80000000, v40
	v_mov_b32_e32 v76, v41
	v_pk_add_f32 v[90:91], v[32:33], v[76:77]
	v_pk_add_f32 v[40:41], v[32:33], v[76:77] neg_lo:[0,1] neg_hi:[0,1]
	v_pk_add_f32 v[76:77], v[54:55], v[48:49]
	v_pk_add_f32 v[48:49], v[54:55], v[48:49] neg_lo:[0,1] neg_hi:[0,1]
	v_pk_add_f32 v[32:33], v[60:61], v[82:83]
	v_pk_add_f32 v[60:61], v[60:61], v[82:83] neg_lo:[0,1] neg_hi:[0,1]
	v_xor_b32_e32 v55, 0x80000000, v48
	v_mov_b32_e32 v54, v49
	v_pk_add_f32 v[82:83], v[32:33], v[76:77]
	v_pk_add_f32 v[48:49], v[32:33], v[76:77] neg_lo:[0,1] neg_hi:[0,1]
	v_pk_add_f32 v[76:77], v[60:61], v[54:55]
	v_pk_add_f32 v[32:33], v[60:61], v[54:55] neg_lo:[0,1] neg_hi:[0,1]
	v_pk_add_f32 v[54:55], v[92:93], v[84:85]
	v_pk_add_f32 v[60:61], v[92:93], v[84:85] neg_lo:[0,1] neg_hi:[0,1]
	v_pk_add_f32 v[84:85], v[56:57], v[44:45]
	v_pk_add_f32 v[44:45], v[44:45], v[56:57] neg_lo:[0,1] neg_hi:[0,1]
	v_pk_add_f32 v[86:87], v[86:87], v[88:89]
	v_xor_b32_e32 v56, 0x80000000, v45
	v_mov_b32_e32 v57, v44
	v_pk_mul_f32 v[56:57], v[10:11], v[56:57] op_sel_hi:[0,1] neg_lo:[1,0] neg_hi:[1,0]
	v_pk_fma_f32 v[56:57], v[10:11], v[44:45], v[56:57] op_sel_hi:[0,1,1]
	v_pk_add_f32 v[44:45], v[80:81], v[58:59]
	v_pk_add_f32 v[58:59], v[80:81], v[58:59] neg_lo:[0,1] neg_hi:[0,1]
	v_xor_b32_e32 v88, 0x80000000, v87
	v_xor_b32_e32 v81, 0x80000000, v58
	v_mov_b32_e32 v80, v59
	v_pk_add_f32 v[58:59], v[52:53], v[36:37]
	v_pk_add_f32 v[36:37], v[52:53], v[36:37] neg_lo:[0,1] neg_hi:[0,1]
	v_mov_b32_e32 v89, v87
	v_xor_b32_e32 v52, 0x80000000, v37
	v_mov_b32_e32 v53, v36
	v_pk_mul_f32 v[52:53], v[10:11], v[52:53] op_sel_hi:[0,1] neg_lo:[1,0] neg_hi:[1,0]
	v_pk_fma_f32 v[36:37], v[10:11], v[36:37], v[52:53] op_sel_hi:[0,1,1] neg_lo:[1,0,0] neg_hi:[1,0,0]
	v_pk_add_f32 v[52:53], v[54:55], v[44:45]
	v_pk_add_f32 v[44:45], v[54:55], v[44:45] neg_lo:[0,1] neg_hi:[0,1]
	v_pk_add_f32 v[54:55], v[84:85], v[58:59]
	v_pk_add_f32 v[58:59], v[84:85], v[58:59] neg_lo:[0,1] neg_hi:[0,1]
	s_nop 0
	v_xor_b32_e32 v85, 0x80000000, v58
	v_mov_b32_e32 v84, v59
	v_pk_add_f32 v[58:59], v[52:53], v[54:55]
	v_pk_add_f32 v[52:53], v[52:53], v[54:55] neg_lo:[0,1] neg_hi:[0,1]
	v_pk_add_f32 v[54:55], v[44:45], v[84:85]
	v_pk_add_f32 v[44:45], v[44:45], v[84:85] neg_lo:[0,1] neg_hi:[0,1]
	v_pk_add_f32 v[84:85], v[60:61], v[80:81]
	v_pk_add_f32 v[60:61], v[60:61], v[80:81] neg_lo:[0,1] neg_hi:[0,1]
	v_pk_add_f32 v[80:81], v[56:57], v[36:37]
	v_pk_add_f32 v[36:37], v[56:57], v[36:37] neg_lo:[0,1] neg_hi:[0,1]
	v_pk_add_f32 v[92:93], v[84:85], v[80:81]
	v_xor_b32_e32 v57, 0x80000000, v36
	v_mov_b32_e32 v56, v37
	v_pk_add_f32 v[80:81], v[84:85], v[80:81] neg_lo:[0,1] neg_hi:[0,1]
	v_pk_add_f32 v[84:85], v[60:61], v[56:57]
	v_pk_add_f32 v[36:37], v[60:61], v[56:57] neg_lo:[0,1] neg_hi:[0,1]
	v_xor_b32_e32 v56, 0x80000000, v95
	v_mov_b32_e32 v57, v95
	v_pk_fma_f32 v[60:61], v[16:17], s[92:93], v[16:17] op_sel:[1,0,0] op_sel_hi:[0,1,1]
	v_pk_mul_f32 v[56:57], v[56:57], s[14:15]
	v_pk_mul_f32 v[88:89], v[60:61], v[88:89] op_sel:[1,0] op_sel_hi:[0,1]
	v_pk_fma_f32 v[56:57], v[94:95], s[42:43], v[56:57] op_sel_hi:[0,1,1]
	v_pk_fma_f32 v[86:87], v[60:61], v[86:87], v[88:89] op_sel_hi:[1,0,1]
	ds_write2_b64 v75, v[56:57], v[86:87] offset1:16
	v_xor_b32_e32 v56, 0x80000000, v61
	v_mov_b32_e32 v57, v61
	v_pk_mul_f32 v[56:57], v[16:17], v[56:57] op_sel:[1,0] op_sel_hi:[0,1]
	v_pk_fma_f32 v[56:57], v[16:17], v[60:61], v[56:57] op_sel_hi:[1,0,1]
	v_xor_b32_e32 v60, 0x80000000, v103
	v_mov_b32_e32 v61, v103
	v_xor_b32_e32 v86, 0x80000000, v57
	v_mov_b32_e32 v87, v57
	v_pk_mul_f32 v[60:61], v[56:57], v[60:61] op_sel:[1,0] op_sel_hi:[0,1]
	v_pk_mul_f32 v[86:87], v[16:17], v[86:87] op_sel:[1,0] op_sel_hi:[0,1]
	v_pk_fma_f32 v[60:61], v[56:57], v[102:103], v[60:61] op_sel_hi:[1,0,1]
	v_pk_fma_f32 v[56:57], v[16:17], v[56:57], v[86:87] op_sel_hi:[1,0,1]
	v_xor_b32_e32 v86, 0x80000000, v59
	v_mov_b32_e32 v87, v59
	v_pk_mul_f32 v[86:87], v[56:57], v[86:87] op_sel:[1,0] op_sel_hi:[0,1]
	v_pk_fma_f32 v[58:59], v[56:57], v[58:59], v[86:87] op_sel_hi:[1,0,1]
	ds_write2_b64 v74, v[60:61], v[58:59] offset0:32 offset1:48
	v_xor_b32_e32 v58, 0x80000000, v57
	v_mov_b32_e32 v59, v57
	v_pk_mul_f32 v[58:59], v[16:17], v[58:59] op_sel:[1,0] op_sel_hi:[0,1]
	v_pk_fma_f32 v[56:57], v[16:17], v[56:57], v[58:59] op_sel_hi:[1,0,1]
	v_xor_b32_e32 v58, 0x80000000, v105
	v_mov_b32_e32 v59, v105
	v_xor_b32_e32 v60, 0x80000000, v57
	v_mov_b32_e32 v61, v57
	v_pk_mul_f32 v[58:59], v[56:57], v[58:59] op_sel:[1,0] op_sel_hi:[0,1]
	v_pk_mul_f32 v[60:61], v[16:17], v[60:61] op_sel:[1,0] op_sel_hi:[0,1]
	v_pk_fma_f32 v[58:59], v[56:57], v[104:105], v[58:59] op_sel_hi:[1,0,1]
	v_pk_fma_f32 v[56:57], v[16:17], v[56:57], v[60:61] op_sel_hi:[1,0,1]
	v_xor_b32_e32 v60, 0x80000000, v83
	v_mov_b32_e32 v61, v83
	v_pk_mul_f32 v[60:61], v[56:57], v[60:61] op_sel:[1,0] op_sel_hi:[0,1]
	v_pk_fma_f32 v[60:61], v[56:57], v[82:83], v[60:61] op_sel_hi:[1,0,1]
	ds_write2_b64 v73, v[58:59], v[60:61] offset0:64 offset1:80
	v_xor_b32_e32 v58, 0x80000000, v57
	v_mov_b32_e32 v59, v57
	v_pk_mul_f32 v[58:59], v[16:17], v[58:59] op_sel:[1,0] op_sel_hi:[0,1]
	v_pk_fma_f32 v[56:57], v[16:17], v[56:57], v[58:59] op_sel_hi:[1,0,1]
	v_xor_b32_e32 v58, 0x80000000, v99
	v_mov_b32_e32 v59, v99
	v_xor_b32_e32 v60, 0x80000000, v57
	v_mov_b32_e32 v61, v57
	v_pk_mul_f32 v[58:59], v[56:57], v[58:59] op_sel:[1,0] op_sel_hi:[0,1]
	v_pk_mul_f32 v[60:61], v[16:17], v[60:61] op_sel:[1,0] op_sel_hi:[0,1]
	v_pk_fma_f32 v[58:59], v[56:57], v[98:99], v[58:59] op_sel_hi:[1,0,1]
	v_pk_fma_f32 v[56:57], v[16:17], v[56:57], v[60:61] op_sel_hi:[1,0,1]
	v_xor_b32_e32 v60, 0x80000000, v93
	v_mov_b32_e32 v61, v93
	v_pk_mul_f32 v[60:61], v[56:57], v[60:61] op_sel:[1,0] op_sel_hi:[0,1]
	v_pk_fma_f32 v[60:61], v[56:57], v[92:93], v[60:61] op_sel_hi:[1,0,1]
	ds_write2_b64 v72, v[58:59], v[60:61] offset0:96 offset1:112
	v_xor_b32_e32 v58, 0x80000000, v57
	v_mov_b32_e32 v59, v57
	v_pk_mul_f32 v[58:59], v[16:17], v[58:59] op_sel:[1,0] op_sel_hi:[0,1]
	v_pk_fma_f32 v[56:57], v[16:17], v[56:57], v[58:59] op_sel_hi:[1,0,1]
	v_xor_b32_e32 v58, 0x80000000, v47
	v_mov_b32_e32 v59, v47
	v_pk_mul_f32 v[58:59], v[56:57], v[58:59] op_sel:[1,0] op_sel_hi:[0,1]
	v_pk_fma_f32 v[46:47], v[56:57], v[46:47], v[58:59] op_sel_hi:[1,0,1]
	v_xor_b32_e32 v58, 0x80000000, v57
	v_mov_b32_e32 v59, v57
	v_pk_mul_f32 v[58:59], v[16:17], v[58:59] op_sel:[1,0] op_sel_hi:[0,1]
	v_pk_fma_f32 v[56:57], v[16:17], v[56:57], v[58:59] op_sel_hi:[1,0,1]
	v_xor_b32_e32 v58, 0x80000000, v91
	v_mov_b32_e32 v59, v91
	v_pk_mul_f32 v[58:59], v[56:57], v[58:59] op_sel:[1,0] op_sel_hi:[0,1]
	v_pk_fma_f32 v[58:59], v[56:57], v[90:91], v[58:59] op_sel_hi:[1,0,1]
	ds_write2_b64 v71, v[46:47], v[58:59] offset0:128 offset1:144
	v_xor_b32_e32 v46, 0x80000000, v57
	v_mov_b32_e32 v47, v57
	v_pk_mul_f32 v[46:47], v[16:17], v[46:47] op_sel:[1,0] op_sel_hi:[0,1]
	v_pk_fma_f32 v[46:47], v[16:17], v[56:57], v[46:47] op_sel_hi:[1,0,1]
	v_xor_b32_e32 v56, 0x80000000, v51
	v_mov_b32_e32 v57, v51
	v_pk_mul_f32 v[56:57], v[46:47], v[56:57] op_sel:[1,0] op_sel_hi:[0,1]
	v_pk_fma_f32 v[50:51], v[46:47], v[50:51], v[56:57] op_sel_hi:[1,0,1]
	v_xor_b32_e32 v56, 0x80000000, v47
	v_mov_b32_e32 v57, v47
	v_pk_mul_f32 v[56:57], v[16:17], v[56:57] op_sel:[1,0] op_sel_hi:[0,1]
	v_pk_fma_f32 v[46:47], v[16:17], v[46:47], v[56:57] op_sel_hi:[1,0,1]
	v_xor_b32_e32 v56, 0x80000000, v55
	v_mov_b32_e32 v57, v55
	v_pk_mul_f32 v[56:57], v[46:47], v[56:57] op_sel:[1,0] op_sel_hi:[0,1]
	v_pk_fma_f32 v[54:55], v[46:47], v[54:55], v[56:57] op_sel_hi:[1,0,1]
	ds_write2_b64 v70, v[50:51], v[54:55] offset0:160 offset1:176
	v_xor_b32_e32 v50, 0x80000000, v47
	v_mov_b32_e32 v51, v47
	v_pk_mul_f32 v[50:51], v[16:17], v[50:51] op_sel:[1,0] op_sel_hi:[0,1]
	v_pk_fma_f32 v[46:47], v[16:17], v[46:47], v[50:51] op_sel_hi:[1,0,1]
	v_xor_b32_e32 v50, 0x80000000, v39
	v_mov_b32_e32 v51, v39
	v_pk_mul_f32 v[50:51], v[50:51], v[46:47] op_sel:[0,1] op_sel_hi:[1,0]
	s_nop 0
	v_pk_fma_f32 v[38:39], v[38:39], v[46:47], v[50:51] op_sel_hi:[0,1,1]
	v_xor_b32_e32 v50, 0x80000000, v47
	v_mov_b32_e32 v51, v47
	v_pk_mul_f32 v[50:51], v[16:17], v[50:51] op_sel:[1,0] op_sel_hi:[0,1]
	v_pk_fma_f32 v[46:47], v[16:17], v[46:47], v[50:51] op_sel_hi:[1,0,1]
	v_xor_b32_e32 v50, 0x80000000, v77
	v_mov_b32_e32 v51, v77
	v_pk_mul_f32 v[50:51], v[46:47], v[50:51] op_sel:[1,0] op_sel_hi:[0,1]
	v_pk_fma_f32 v[50:51], v[46:47], v[76:77], v[50:51] op_sel_hi:[1,0,1]
	ds_write2_b64 v69, v[38:39], v[50:51] offset0:192 offset1:208
	v_xor_b32_e32 v38, 0x80000000, v47
	v_mov_b32_e32 v39, v47
	v_pk_mul_f32 v[38:39], v[16:17], v[38:39] op_sel:[1,0] op_sel_hi:[0,1]
	v_pk_fma_f32 v[38:39], v[16:17], v[46:47], v[38:39] op_sel_hi:[1,0,1]
	v_xor_b32_e32 v46, 0x80000000, v43
	v_mov_b32_e32 v47, v43
	v_pk_mul_f32 v[46:47], v[46:47], v[38:39] op_sel:[0,1] op_sel_hi:[1,0]
	s_nop 0
	v_pk_fma_f32 v[42:43], v[42:43], v[38:39], v[46:47] op_sel_hi:[0,1,1]
	v_xor_b32_e32 v46, 0x80000000, v39
	v_mov_b32_e32 v47, v39
	v_pk_mul_f32 v[46:47], v[16:17], v[46:47] op_sel:[1,0] op_sel_hi:[0,1]
	v_pk_fma_f32 v[38:39], v[16:17], v[38:39], v[46:47] op_sel_hi:[1,0,1]
	v_xor_b32_e32 v46, 0x80000000, v85
	v_mov_b32_e32 v47, v85
	v_pk_mul_f32 v[46:47], v[38:39], v[46:47] op_sel:[1,0] op_sel_hi:[0,1]
	v_pk_fma_f32 v[46:47], v[38:39], v[84:85], v[46:47] op_sel_hi:[1,0,1]
	ds_write2_b64 v68, v[42:43], v[46:47] offset0:224 offset1:240
	v_xor_b32_e32 v42, 0x80000000, v39
	v_mov_b32_e32 v43, v39
	v_pk_mul_f32 v[42:43], v[16:17], v[42:43] op_sel:[1,0] op_sel_hi:[0,1]
	v_pk_fma_f32 v[38:39], v[16:17], v[38:39], v[42:43] op_sel_hi:[1,0,1]
	v_xor_b32_e32 v42, 0x80000000, v31
	v_mov_b32_e32 v43, v31
	v_pk_mul_f32 v[42:43], v[42:43], v[38:39] op_sel:[0,1] op_sel_hi:[1,0]
	s_nop 0
	v_pk_fma_f32 v[30:31], v[30:31], v[38:39], v[42:43] op_sel_hi:[0,1,1]
	v_xor_b32_e32 v42, 0x80000000, v39
	v_mov_b32_e32 v43, v39
	v_pk_mul_f32 v[42:43], v[16:17], v[42:43] op_sel:[1,0] op_sel_hi:[0,1]
	v_pk_fma_f32 v[38:39], v[16:17], v[38:39], v[42:43] op_sel_hi:[1,0,1]
	v_xor_b32_e32 v42, 0x80000000, v79
	v_mov_b32_e32 v43, v79
	v_pk_mul_f32 v[42:43], v[42:43], v[38:39] op_sel:[0,1] op_sel_hi:[1,0]
	s_nop 0
	v_pk_fma_f32 v[42:43], v[78:79], v[38:39], v[42:43] op_sel_hi:[0,1,1]
	ds_write2_b64 v67, v[30:31], v[42:43] offset1:16
	v_xor_b32_e32 v30, 0x80000000, v39
	v_mov_b32_e32 v31, v39
	v_pk_mul_f32 v[30:31], v[16:17], v[30:31] op_sel:[1,0] op_sel_hi:[0,1]
	v_pk_fma_f32 v[30:31], v[16:17], v[38:39], v[30:31] op_sel_hi:[1,0,1]
	v_xor_b32_e32 v38, 0x80000000, v35
	v_mov_b32_e32 v39, v35
	v_pk_mul_f32 v[38:39], v[38:39], v[30:31] op_sel:[0,1] op_sel_hi:[1,0]
	s_nop 0
	v_pk_fma_f32 v[34:35], v[34:35], v[30:31], v[38:39] op_sel_hi:[0,1,1]
	v_xor_b32_e32 v38, 0x80000000, v31
	v_mov_b32_e32 v39, v31
	v_pk_mul_f32 v[38:39], v[16:17], v[38:39] op_sel:[1,0] op_sel_hi:[0,1]
	v_pk_fma_f32 v[30:31], v[16:17], v[30:31], v[38:39] op_sel_hi:[1,0,1]
	v_xor_b32_e32 v38, 0x80000000, v53
	v_mov_b32_e32 v39, v53
	v_pk_mul_f32 v[38:39], v[38:39], v[30:31] op_sel:[0,1] op_sel_hi:[1,0]
	s_nop 0
	v_pk_fma_f32 v[38:39], v[52:53], v[30:31], v[38:39] op_sel_hi:[0,1,1]
	ds_write2_b64 v66, v[34:35], v[38:39] offset0:32 offset1:48
	v_xor_b32_e32 v34, 0x80000000, v31
	v_mov_b32_e32 v35, v31
	v_pk_mul_f32 v[34:35], v[16:17], v[34:35] op_sel:[1,0] op_sel_hi:[0,1]
	v_pk_fma_f32 v[30:31], v[16:17], v[30:31], v[34:35] op_sel_hi:[1,0,1]
	v_xor_b32_e32 v34, 0x80000000, v27
	v_mov_b32_e32 v35, v27
	v_pk_mul_f32 v[34:35], v[34:35], v[30:31] op_sel:[0,1] op_sel_hi:[1,0]
	s_nop 0
	v_pk_fma_f32 v[26:27], v[26:27], v[30:31], v[34:35] op_sel_hi:[0,1,1]
	v_xor_b32_e32 v34, 0x80000000, v31
	v_mov_b32_e32 v35, v31
	v_pk_mul_f32 v[34:35], v[16:17], v[34:35] op_sel:[1,0] op_sel_hi:[0,1]
	v_pk_fma_f32 v[30:31], v[16:17], v[30:31], v[34:35] op_sel_hi:[1,0,1]
	v_xor_b32_e32 v34, 0x80000000, v49
	v_mov_b32_e32 v35, v49
	v_pk_mul_f32 v[34:35], v[34:35], v[30:31] op_sel:[0,1] op_sel_hi:[1,0]
	s_nop 0
	v_pk_fma_f32 v[34:35], v[48:49], v[30:31], v[34:35] op_sel_hi:[0,1,1]
	ds_write2_b64 v65, v[26:27], v[34:35] offset0:64 offset1:80
	v_xor_b32_e32 v26, 0x80000000, v31
	v_mov_b32_e32 v27, v31
	v_pk_mul_f32 v[26:27], v[16:17], v[26:27] op_sel:[1,0] op_sel_hi:[0,1]
	v_pk_fma_f32 v[26:27], v[16:17], v[30:31], v[26:27] op_sel_hi:[1,0,1]
	v_xor_b32_e32 v30, 0x80000000, v29
	v_mov_b32_e32 v31, v29
	v_pk_mul_f32 v[30:31], v[30:31], v[26:27] op_sel:[0,1] op_sel_hi:[1,0]
	s_nop 0
	v_pk_fma_f32 v[28:29], v[28:29], v[26:27], v[30:31] op_sel_hi:[0,1,1]
	v_xor_b32_e32 v30, 0x80000000, v27
	v_mov_b32_e32 v31, v27
	v_pk_mul_f32 v[30:31], v[16:17], v[30:31] op_sel:[1,0] op_sel_hi:[0,1]
	v_pk_fma_f32 v[26:27], v[16:17], v[26:27], v[30:31] op_sel_hi:[1,0,1]
	v_xor_b32_e32 v30, 0x80000000, v81
	v_mov_b32_e32 v31, v81
	v_pk_mul_f32 v[30:31], v[30:31], v[26:27] op_sel:[0,1] op_sel_hi:[1,0]
	s_nop 0
	v_pk_fma_f32 v[30:31], v[80:81], v[26:27], v[30:31] op_sel_hi:[0,1,1]
	ds_write2_b64 v64, v[28:29], v[30:31] offset0:96 offset1:112
	v_xor_b32_e32 v28, 0x80000000, v27
	v_mov_b32_e32 v29, v27
	v_pk_mul_f32 v[28:29], v[16:17], v[28:29] op_sel:[1,0] op_sel_hi:[0,1]
	v_pk_fma_f32 v[26:27], v[16:17], v[26:27], v[28:29] op_sel_hi:[1,0,1]
	v_xor_b32_e32 v28, 0x80000000, v23
	v_mov_b32_e32 v29, v23
	v_pk_mul_f32 v[28:29], v[28:29], v[26:27] op_sel:[0,1] op_sel_hi:[1,0]
	s_nop 0
	v_pk_fma_f32 v[22:23], v[22:23], v[26:27], v[28:29] op_sel_hi:[0,1,1]
	v_xor_b32_e32 v28, 0x80000000, v27
	v_mov_b32_e32 v29, v27
	v_pk_mul_f32 v[28:29], v[16:17], v[28:29] op_sel:[1,0] op_sel_hi:[0,1]
	v_pk_fma_f32 v[26:27], v[16:17], v[26:27], v[28:29] op_sel_hi:[1,0,1]
	v_xor_b32_e32 v28, 0x80000000, v41
	v_mov_b32_e32 v29, v41
	v_pk_mul_f32 v[28:29], v[28:29], v[26:27] op_sel:[0,1] op_sel_hi:[1,0]
	s_nop 0
	v_pk_fma_f32 v[28:29], v[40:41], v[26:27], v[28:29] op_sel_hi:[0,1,1]
	ds_write2_b64 v63, v[22:23], v[28:29] offset0:128 offset1:144
	v_xor_b32_e32 v22, 0x80000000, v27
	v_mov_b32_e32 v23, v27
	v_pk_mul_f32 v[22:23], v[16:17], v[22:23] op_sel:[1,0] op_sel_hi:[0,1]
	v_pk_fma_f32 v[22:23], v[16:17], v[26:27], v[22:23] op_sel_hi:[1,0,1]
	v_xor_b32_e32 v26, 0x80000000, v25
	v_mov_b32_e32 v27, v25
	v_pk_mul_f32 v[26:27], v[26:27], v[22:23] op_sel:[0,1] op_sel_hi:[1,0]
	s_nop 0
	v_pk_fma_f32 v[24:25], v[24:25], v[22:23], v[26:27] op_sel_hi:[0,1,1]
	v_xor_b32_e32 v26, 0x80000000, v23
	v_mov_b32_e32 v27, v23
	v_pk_mul_f32 v[26:27], v[16:17], v[26:27] op_sel:[1,0] op_sel_hi:[0,1]
	v_pk_fma_f32 v[22:23], v[16:17], v[22:23], v[26:27] op_sel_hi:[1,0,1]
	v_xor_b32_e32 v26, 0x80000000, v45
	v_mov_b32_e32 v27, v45
	v_pk_mul_f32 v[26:27], v[26:27], v[22:23] op_sel:[0,1] op_sel_hi:[1,0]
	s_nop 0
	v_pk_fma_f32 v[26:27], v[44:45], v[22:23], v[26:27] op_sel_hi:[0,1,1]
	ds_write2_b64 v62, v[24:25], v[26:27] offset0:160 offset1:176
	v_xor_b32_e32 v24, 0x80000000, v23
	v_mov_b32_e32 v25, v23
	v_pk_mul_f32 v[24:25], v[16:17], v[24:25] op_sel:[1,0] op_sel_hi:[0,1]
	v_pk_fma_f32 v[22:23], v[16:17], v[22:23], v[24:25] op_sel_hi:[1,0,1]
	v_xor_b32_e32 v24, 0x80000000, v19
	v_mov_b32_e32 v25, v19
	v_pk_mul_f32 v[24:25], v[24:25], v[22:23] op_sel:[0,1] op_sel_hi:[1,0]
	s_nop 0
	v_pk_fma_f32 v[18:19], v[18:19], v[22:23], v[24:25] op_sel_hi:[0,1,1]
	v_xor_b32_e32 v24, 0x80000000, v23
	v_mov_b32_e32 v25, v23
	v_pk_mul_f32 v[24:25], v[16:17], v[24:25] op_sel:[1,0] op_sel_hi:[0,1]
	v_pk_fma_f32 v[22:23], v[16:17], v[22:23], v[24:25] op_sel_hi:[1,0,1]
	v_xor_b32_e32 v24, 0x80000000, v33
	v_mov_b32_e32 v25, v33
	v_pk_mul_f32 v[24:25], v[24:25], v[22:23] op_sel:[0,1] op_sel_hi:[1,0]
	s_nop 0
	v_pk_fma_f32 v[24:25], v[32:33], v[22:23], v[24:25] op_sel_hi:[0,1,1]
	ds_write2_b64 v15, v[18:19], v[24:25] offset0:192 offset1:208
	v_xor_b32_e32 v18, 0x80000000, v23
	v_mov_b32_e32 v19, v23
	v_pk_mul_f32 v[18:19], v[16:17], v[18:19] op_sel:[1,0] op_sel_hi:[0,1]
	v_pk_fma_f32 v[18:19], v[16:17], v[22:23], v[18:19] op_sel_hi:[1,0,1]
	v_xor_b32_e32 v22, 0x80000000, v21
	v_mov_b32_e32 v23, v21
	v_pk_mul_f32 v[22:23], v[22:23], v[18:19] op_sel:[0,1] op_sel_hi:[1,0]
	s_nop 0
	v_pk_fma_f32 v[20:21], v[20:21], v[18:19], v[22:23] op_sel_hi:[0,1,1]
	v_xor_b32_e32 v22, 0x80000000, v19
	v_mov_b32_e32 v23, v19
	v_pk_mul_f32 v[22:23], v[16:17], v[22:23] op_sel:[1,0] op_sel_hi:[0,1]
	v_pk_fma_f32 v[16:17], v[16:17], v[18:19], v[22:23] op_sel_hi:[1,0,1]
	v_xor_b32_e32 v18, 0x80000000, v37
	v_mov_b32_e32 v19, v37
	v_pk_mul_f32 v[18:19], v[18:19], v[16:17] op_sel:[0,1] op_sel_hi:[1,0]
	s_nop 0
	v_pk_fma_f32 v[16:17], v[36:37], v[16:17], v[18:19] op_sel_hi:[0,1,1]
	ds_write2_b64 v13, v[20:21], v[16:17] offset0:224 offset1:240
	v_mov_b32_e32 v16, v1
	v_mov_b32_e32 v10, v178
	v_mov_b32_e32 v17, v177
	s_waitcnt lgkmcnt(0)
	s_barrier
	v_lshlrev_b32_e32 v190, 3, v16
	v_add_u32_e32 v190, 0x1000, v190
	global_load_dwordx2 v[196:197], v190, s[48:49] offset:-4096
	global_load_dwordx2 v[198:199], v190, s[48:49]
	v_add_u32_e32 v190, 0x2000, v190
	global_load_dwordx2 v[200:201], v190, s[48:49] offset:-4096
	global_load_dwordx2 v[202:203], v190, s[48:49]
	v_add_u32_e32 v190, 0x2000, v190
	global_load_dwordx2 v[204:205], v190, s[48:49] offset:-4096
	global_load_dwordx2 v[206:207], v190, s[48:49]
	v_add_u32_e32 v190, 0x2000, v190
	global_load_dwordx2 v[208:209], v190, s[48:49] offset:-4096
	global_load_dwordx2 v[210:211], v190, s[48:49]
	v_add_u32_e32 v190, 0x2000, v190
	global_load_dwordx2 v[212:213], v190, s[48:49] offset:-4096
	global_load_dwordx2 v[214:215], v190, s[48:49]
	v_add_u32_e32 v190, 0x2000, v190
	global_load_dwordx2 v[216:217], v190, s[48:49] offset:-4096
	global_load_dwordx2 v[218:219], v190, s[48:49]
	v_add_u32_e32 v190, 0x2000, v190
	global_load_dwordx2 v[220:221], v190, s[48:49] offset:-4096
	global_load_dwordx2 v[222:223], v190, s[48:49]
	v_add_u32_e32 v190, 0x2000, v190
	global_load_dwordx2 v[224:225], v190, s[48:49] offset:-4096
	global_load_dwordx2 v[226:227], v190, s[48:49]
	v_mov_b32_e32 v50, v166
	v_lshlrev_b32_e32 v13, 3, v17
	v_lshlrev_b32_e32 v48, 3, v10
	v_add3_u32 v10, 0, v13, v48
	v_xor_b32_e32 v13, 1, v17
	v_xor_b32_e32 v34, 8, v17
	v_xor_b32_e32 v36, 9, v17
	v_lshlrev_b32_e32 v13, 3, v13
	v_xor_b32_e32 v15, 2, v17
	v_xor_b32_e32 v24, 3, v17
	v_xor_b32_e32 v26, 4, v17
	v_xor_b32_e32 v28, 5, v17
	v_xor_b32_e32 v30, 6, v17
	v_xor_b32_e32 v32, 7, v17
	v_lshlrev_b32_e32 v34, 3, v34
	v_lshlrev_b32_e32 v36, 3, v36
	v_xor_b32_e32 v38, 10, v17
	v_xor_b32_e32 v40, 11, v17
	v_xor_b32_e32 v42, 12, v17
	v_xor_b32_e32 v44, 13, v17
	v_xor_b32_e32 v46, 14, v17
	v_xor_b32_e32 v17, 15, v17
	v_add3_u32 v13, 0, v13, v48
	v_lshlrev_b32_e32 v15, 3, v15
	v_lshlrev_b32_e32 v24, 3, v24
	v_lshlrev_b32_e32 v26, 3, v26
	v_lshlrev_b32_e32 v28, 3, v28
	v_lshlrev_b32_e32 v30, 3, v30
	v_lshlrev_b32_e32 v32, 3, v32
	v_add3_u32 v57, 0, v34, v48
	v_add3_u32 v58, 0, v36, v48
	v_lshlrev_b32_e32 v38, 3, v38
	v_lshlrev_b32_e32 v40, 3, v40
	v_lshlrev_b32_e32 v42, 3, v42
	v_lshlrev_b32_e32 v44, 3, v44
	v_lshlrev_b32_e32 v46, 3, v46
	v_lshlrev_b32_e32 v17, 3, v17
	ds_read_b64 v[18:19], v10
	ds_read_b64 v[20:21], v13
	v_add3_u32 v15, 0, v15, v48
	v_add3_u32 v52, 0, v24, v48
	v_add3_u32 v53, 0, v26, v48
	v_add3_u32 v54, 0, v28, v48
	v_add3_u32 v55, 0, v30, v48
	v_add3_u32 v56, 0, v32, v48
	ds_read_b64 v[34:35], v57
	ds_read_b64 v[36:37], v58
	v_add3_u32 v59, 0, v38, v48
	v_add3_u32 v60, 0, v40, v48
	v_add3_u32 v61, 0, v42, v48
	v_add3_u32 v62, 0, v44, v48
	v_add3_u32 v63, 0, v46, v48
	v_add3_u32 v64, 0, v17, v48
	v_mov_b32_e32 v17, v164
	ds_read_b64 v[22:23], v15
	ds_read_b64 v[24:25], v52
	ds_read_b64 v[26:27], v53
	ds_read_b64 v[28:29], v54
	ds_read_b64 v[30:31], v55
	ds_read_b64 v[32:33], v56
	ds_read_b64 v[38:39], v59
	ds_read_b64 v[40:41], v60
	ds_read_b64 v[42:43], v61
	ds_read_b64 v[44:45], v62
	ds_read_b64 v[46:47], v63
	ds_read_b64 v[48:49], v64
	s_waitcnt lgkmcnt(13)
	v_pk_add_f32 v[70:71], v[18:19], v[34:35]
	v_mov_b32_e32 v17, v165
	v_pk_add_f32 v[18:19], v[18:19], v[34:35] neg_lo:[0,1] neg_hi:[0,1]
	v_mov_b32_e32 v17, v167
	s_waitcnt lgkmcnt(12)
	v_pk_add_f32 v[34:35], v[20:21], v[36:37]
	v_pk_add_f32 v[20:21], v[20:21], v[36:37] neg_lo:[0,1] neg_hi:[0,1]
	v_mov_b32_e32 v66, v168
	v_mov_b32_e32 v17, v169
	v_mov_b32_e32 v68, v170
	v_xor_b32_e32 v36, 0x80000000, v21
	v_mov_b32_e32 v37, v20
	s_nop 0
	v_pk_mul_f32 v[36:37], v[36:37], v[68:69] op_sel_hi:[1,0] neg_lo:[0,1] neg_hi:[0,1]
	v_mov_b32_e32 v17, v171
	v_pk_fma_f32 v[20:21], v[20:21], v[50:51], v[36:37] op_sel_hi:[1,0,1]
	s_waitcnt lgkmcnt(5)
	v_pk_add_f32 v[36:37], v[22:23], v[38:39]
	v_pk_add_f32 v[22:23], v[22:23], v[38:39] neg_lo:[0,1] neg_hi:[0,1]
	s_nop 0
	v_xor_b32_e32 v38, 0x80000000, v23
	v_mov_b32_e32 v39, v22
	v_pk_mul_f32 v[38:39], v[38:39], v[66:67] op_sel_hi:[1,0] neg_lo:[0,1] neg_hi:[0,1]
	v_mov_b32_e32 v17, v172
	v_pk_fma_f32 v[22:23], v[22:23], v[66:67], v[38:39] op_sel_hi:[1,0,1]
	s_waitcnt lgkmcnt(4)
	v_pk_add_f32 v[38:39], v[24:25], v[40:41]
	v_pk_add_f32 v[24:25], v[24:25], v[40:41] neg_lo:[0,1] neg_hi:[0,1]
	s_nop 0
	v_pk_mul_f32 v[40:41], v[24:25], v[68:69] op_sel_hi:[1,0]
	v_xor_b32_e32 v72, 0x80000000, v25
	v_mov_b32_e32 v73, v24
	v_pk_fma_f32 v[24:25], v[72:73], v[50:51], v[40:41] op_sel_hi:[1,0,1] neg_lo:[0,1,0] neg_hi:[0,1,0]
	s_waitcnt lgkmcnt(3)
	v_pk_add_f32 v[40:41], v[26:27], v[42:43]
	v_pk_add_f32 v[26:27], v[26:27], v[42:43] neg_lo:[0,1] neg_hi:[0,1]
	v_ashrrev_i32_e32 v17, 31, v16
	v_xor_b32_e32 v73, 0x80000000, v26
	v_mov_b32_e32 v72, v27
	s_waitcnt lgkmcnt(2)
	v_pk_add_f32 v[26:27], v[28:29], v[44:45]
	v_pk_add_f32 v[28:29], v[28:29], v[44:45] neg_lo:[0,1] neg_hi:[0,1]
	s_nop 0
	v_pk_mul_f32 v[42:43], v[28:29], v[68:69] op_sel_hi:[1,0] neg_lo:[0,1] neg_hi:[0,1]
	v_xor_b32_e32 v44, 0x80000000, v29
	v_mov_b32_e32 v45, v28
	v_pk_fma_f32 v[28:29], v[44:45], v[50:51], v[42:43] op_sel_hi:[1,0,1] neg_lo:[0,1,0] neg_hi:[0,1,0]
	s_waitcnt lgkmcnt(1)
	v_pk_add_f32 v[42:43], v[30:31], v[46:47]
	v_pk_add_f32 v[30:31], v[30:31], v[46:47] neg_lo:[0,1] neg_hi:[0,1]
	s_nop 0
	v_xor_b32_e32 v44, 0x80000000, v31
	v_mov_b32_e32 v45, v30
	v_pk_mul_f32 v[44:45], v[44:45], v[66:67] op_sel_hi:[1,0] neg_lo:[0,1] neg_hi:[0,1]
	s_nop 0
	v_pk_fma_f32 v[30:31], v[30:31], v[66:67], v[44:45] op_sel_hi:[1,0,1] neg_lo:[0,1,0] neg_hi:[0,1,0]
	s_waitcnt lgkmcnt(0)
	v_pk_add_f32 v[44:45], v[32:33], v[48:49]
	v_pk_add_f32 v[32:33], v[32:33], v[48:49] neg_lo:[0,1] neg_hi:[0,1]
	v_pk_add_f32 v[48:49], v[34:35], v[26:27]
	v_pk_add_f32 v[26:27], v[34:35], v[26:27] neg_lo:[0,1] neg_hi:[0,1]
	v_xor_b32_e32 v46, 0x80000000, v33
	v_xor_b32_e32 v34, 0x80000000, v27
	v_mov_b32_e32 v35, v26
	v_pk_mul_f32 v[34:35], v[34:35], v[66:67] op_sel_hi:[1,0] neg_lo:[0,1] neg_hi:[0,1]
	v_mov_b32_e32 v47, v32
	v_pk_fma_f32 v[26:27], v[26:27], v[66:67], v[34:35] op_sel_hi:[1,0,1]
	v_pk_add_f32 v[34:35], v[36:37], v[42:43]
	v_pk_add_f32 v[36:37], v[36:37], v[42:43] neg_lo:[0,1] neg_hi:[0,1]
	v_pk_mul_f32 v[46:47], v[46:47], v[68:69] op_sel_hi:[1,0] neg_lo:[0,1] neg_hi:[0,1]
	v_xor_b32_e32 v43, 0x80000000, v36
	v_mov_b32_e32 v42, v37
	v_pk_add_f32 v[36:37], v[38:39], v[44:45]
	v_pk_add_f32 v[38:39], v[38:39], v[44:45] neg_lo:[0,1] neg_hi:[0,1]
	v_pk_fma_f32 v[46:47], v[32:33], v[50:51], v[46:47] op_sel_hi:[1,0,1] neg_lo:[0,1,0] neg_hi:[0,1,0]
	v_xor_b32_e32 v44, 0x80000000, v39
	v_mov_b32_e32 v45, v38
	v_pk_add_f32 v[32:33], v[70:71], v[40:41]
	v_pk_mul_f32 v[44:45], v[44:45], v[66:67] op_sel_hi:[1,0] neg_lo:[0,1] neg_hi:[0,1]
	v_pk_add_f32 v[40:41], v[70:71], v[40:41] neg_lo:[0,1] neg_hi:[0,1]
	v_pk_fma_f32 v[38:39], v[38:39], v[66:67], v[44:45] op_sel_hi:[1,0,1] neg_lo:[0,1,0] neg_hi:[0,1,0]
	v_pk_add_f32 v[44:45], v[32:33], v[34:35]
	v_pk_add_f32 v[32:33], v[32:33], v[34:35] neg_lo:[0,1] neg_hi:[0,1]
	v_pk_add_f32 v[34:35], v[48:49], v[36:37]
	v_pk_add_f32 v[36:37], v[48:49], v[36:37] neg_lo:[0,1] neg_hi:[0,1]
	v_pk_add_f32 v[50:51], v[44:45], v[34:35]
	v_xor_b32_e32 v49, 0x80000000, v36
	v_mov_b32_e32 v48, v37
	v_pk_add_f32 v[36:37], v[44:45], v[34:35] neg_lo:[0,1] neg_hi:[0,1]
	v_pk_add_f32 v[68:69], v[32:33], v[48:49]
	v_pk_add_f32 v[44:45], v[32:33], v[48:49] neg_lo:[0,1] neg_hi:[0,1]
	v_pk_add_f32 v[32:33], v[40:41], v[42:43]
	v_pk_add_f32 v[34:35], v[40:41], v[42:43] neg_lo:[0,1] neg_hi:[0,1]
	v_pk_add_f32 v[40:41], v[26:27], v[38:39]
	v_pk_add_f32 v[26:27], v[26:27], v[38:39] neg_lo:[0,1] neg_hi:[0,1]
	v_pk_add_f32 v[42:43], v[32:33], v[40:41] neg_lo:[0,1] neg_hi:[0,1]
	v_xor_b32_e32 v39, 0x80000000, v26
	v_mov_b32_e32 v38, v27
	v_pk_add_f32 v[26:27], v[32:33], v[40:41]
	v_pk_add_f32 v[40:41], v[20:21], v[28:29]
	v_pk_add_f32 v[20:21], v[20:21], v[28:29] neg_lo:[0,1] neg_hi:[0,1]
	v_pk_add_f32 v[32:33], v[34:35], v[38:39]
	v_xor_b32_e32 v28, 0x80000000, v21
	v_mov_b32_e32 v29, v20
	v_pk_mul_f32 v[28:29], v[66:67], v[28:29] op_sel_hi:[0,1] neg_lo:[1,0] neg_hi:[1,0]
	v_pk_fma_f32 v[20:21], v[66:67], v[20:21], v[28:29] op_sel_hi:[0,1,1]
	v_pk_add_f32 v[28:29], v[22:23], v[30:31]
	v_pk_add_f32 v[22:23], v[22:23], v[30:31] neg_lo:[0,1] neg_hi:[0,1]
	v_pk_add_f32 v[38:39], v[34:35], v[38:39] neg_lo:[0,1] neg_hi:[0,1]
	v_xor_b32_e32 v31, 0x80000000, v22
	v_mov_b32_e32 v30, v23
	v_pk_add_f32 v[22:23], v[24:25], v[46:47]
	v_pk_add_f32 v[24:25], v[24:25], v[46:47] neg_lo:[0,1] neg_hi:[0,1]
	v_pk_add_f32 v[34:35], v[18:19], v[72:73]
	v_xor_b32_e32 v46, 0x80000000, v25
	v_mov_b32_e32 v47, v24
	v_pk_mul_f32 v[46:47], v[66:67], v[46:47] op_sel_hi:[0,1] neg_lo:[1,0] neg_hi:[1,0]
	v_pk_fma_f32 v[24:25], v[66:67], v[24:25], v[46:47] op_sel_hi:[0,1,1] neg_lo:[1,0,0] neg_hi:[1,0,0]
	v_pk_add_f32 v[46:47], v[34:35], v[28:29]
	v_pk_add_f32 v[28:29], v[34:35], v[28:29] neg_lo:[0,1] neg_hi:[0,1]
	v_pk_add_f32 v[34:35], v[40:41], v[22:23]
	v_pk_add_f32 v[22:23], v[40:41], v[22:23] neg_lo:[0,1] neg_hi:[0,1]
	v_pk_add_f32 v[18:19], v[18:19], v[72:73] neg_lo:[0,1] neg_hi:[0,1]
	v_xor_b32_e32 v49, 0x80000000, v22
	v_mov_b32_e32 v48, v23
	v_pk_add_f32 v[66:67], v[28:29], v[48:49]
	v_pk_add_f32 v[48:49], v[28:29], v[48:49] neg_lo:[0,1] neg_hi:[0,1]
	v_pk_add_f32 v[28:29], v[18:19], v[30:31]
	v_pk_add_f32 v[18:19], v[18:19], v[30:31] neg_lo:[0,1] neg_hi:[0,1]
	v_pk_add_f32 v[30:31], v[20:21], v[24:25]
	v_pk_add_f32 v[20:21], v[20:21], v[24:25] neg_lo:[0,1] neg_hi:[0,1]
	v_pk_add_f32 v[22:23], v[46:47], v[34:35]
	v_xor_b32_e32 v25, 0x80000000, v20
	v_mov_b32_e32 v24, v21
	v_lshl_add_u64 v[20:21], v[16:17], 3, s[48:49]
	s_waitcnt vmcnt(0)
	v_mov_b32_e32 v20, v196
	v_mov_b32_e32 v21, v197
	v_pk_add_f32 v[40:41], v[46:47], v[34:35] neg_lo:[0,1] neg_hi:[0,1]
	v_pk_add_f32 v[34:35], v[18:19], v[24:25]
	v_pk_add_f32 v[18:19], v[18:19], v[24:25] neg_lo:[0,1] neg_hi:[0,1]
	v_xor_b32_e32 v24, 0x80000000, v51
	v_mov_b32_e32 v25, v51
	v_pk_add_f32 v[70:71], v[28:29], v[30:31]
	v_pk_add_f32 v[46:47], v[28:29], v[30:31] neg_lo:[0,1] neg_hi:[0,1]
	v_xor_b32_e32 v28, 0x80000000, v23
	v_mov_b32_e32 v29, v23
	v_xor_b32_e32 v30, 0x80000000, v69
	v_mov_b32_e32 v31, v69
	v_mov_b32_e32 v17, v164
	s_nop 0
	v_pk_mul_f32 v[24:25], v[24:25], v[20:21] op_sel:[0,1] op_sel_hi:[1,0]
	s_nop 0
	v_pk_fma_f32 v[20:21], v[50:51], v[20:21], v[24:25] op_sel_hi:[0,1,1]
	v_add_u32_e32 v24, 0x200, v16
	v_ashrrev_i32_e32 v25, 31, v24
	v_lshl_add_u64 v[24:25], v[24:25], 3, s[48:49]
	v_mov_b32_e32 v24, v198
	v_mov_b32_e32 v25, v199
	v_xor_b32_e32 v50, 0x80000000, v67
	v_mov_b32_e32 v51, v67
	s_nop 0
	v_pk_mul_f32 v[28:29], v[24:25], v[28:29] op_sel:[1,0] op_sel_hi:[0,1]
	v_pk_fma_f32 v[22:23], v[24:25], v[22:23], v[28:29] op_sel_hi:[1,0,1]
	v_add_u32_e32 v24, 0x400, v16
	v_ashrrev_i32_e32 v25, 31, v24
	v_lshl_add_u64 v[24:25], v[24:25], 3, s[48:49]
	v_mov_b32_e32 v24, v200
	v_mov_b32_e32 v25, v201
	v_xor_b32_e32 v28, 0x80000000, v27
	v_mov_b32_e32 v29, v27
	s_nop 0
	v_pk_mul_f32 v[28:29], v[28:29], v[24:25] op_sel:[0,1] op_sel_hi:[1,0]
	s_nop 0
	v_pk_fma_f32 v[24:25], v[26:27], v[24:25], v[28:29] op_sel_hi:[0,1,1]
	v_add_u32_e32 v26, 0x600, v16
	v_ashrrev_i32_e32 v27, 31, v26
	v_lshl_add_u64 v[26:27], v[26:27], 3, s[48:49]
	v_mov_b32_e32 v26, v202
	v_mov_b32_e32 v27, v203
	v_xor_b32_e32 v28, 0x80000000, v71
	v_mov_b32_e32 v29, v71
	s_nop 0
	v_pk_mul_f32 v[28:29], v[26:27], v[28:29] op_sel:[1,0] op_sel_hi:[0,1]
	v_pk_fma_f32 v[26:27], v[26:27], v[70:71], v[28:29] op_sel_hi:[1,0,1]
	v_add_u32_e32 v28, 0x800, v16
	v_ashrrev_i32_e32 v29, 31, v28
	v_lshl_add_u64 v[28:29], v[28:29], 3, s[48:49]
	v_mov_b32_e32 v28, v204
	v_mov_b32_e32 v29, v205
	s_nop 0
	v_pk_mul_f32 v[30:31], v[30:31], v[28:29] op_sel:[0,1] op_sel_hi:[1,0]
	s_nop 0
	v_pk_fma_f32 v[28:29], v[68:69], v[28:29], v[30:31] op_sel_hi:[0,1,1]
	v_add_u32_e32 v30, 0xa00, v16
	v_ashrrev_i32_e32 v31, 31, v30
	v_lshl_add_u64 v[30:31], v[30:31], 3, s[48:49]
	v_mov_b32_e32 v30, v206
	v_mov_b32_e32 v31, v207
	v_mov_b32_e32 v68, v170
	s_nop 0
	v_pk_mul_f32 v[50:51], v[30:31], v[50:51] op_sel:[1,0] op_sel_hi:[0,1]
	v_pk_fma_f32 v[30:31], v[30:31], v[66:67], v[50:51] op_sel_hi:[1,0,1]
	v_add_u32_e32 v50, 0xc00, v16
	v_ashrrev_i32_e32 v51, 31, v50
	v_lshl_add_u64 v[50:51], v[50:51], 3, s[48:49]
	v_mov_b32_e32 v50, v208
	v_mov_b32_e32 v51, v209
	v_xor_b32_e32 v66, 0x80000000, v33
	v_mov_b32_e32 v67, v33
	s_nop 0
	v_pk_mul_f32 v[66:67], v[66:67], v[50:51] op_sel:[0,1] op_sel_hi:[1,0]
	s_nop 0
	v_pk_fma_f32 v[32:33], v[32:33], v[50:51], v[66:67] op_sel_hi:[0,1,1]
	v_add_u32_e32 v50, 0xe00, v16
	v_ashrrev_i32_e32 v51, 31, v50
	v_lshl_add_u64 v[50:51], v[50:51], 3, s[48:49]
	v_mov_b32_e32 v50, v210
	v_mov_b32_e32 v51, v211
	v_xor_b32_e32 v66, 0x80000000, v35
	v_mov_b32_e32 v67, v35
	s_nop 0
	v_pk_mul_f32 v[66:67], v[50:51], v[66:67] op_sel:[1,0] op_sel_hi:[0,1]
	v_pk_fma_f32 v[34:35], v[50:51], v[34:35], v[66:67] op_sel_hi:[1,0,1]
	v_add_u32_e32 v50, 0x1000, v16
	v_ashrrev_i32_e32 v51, 31, v50
	v_lshl_add_u64 v[50:51], v[50:51], 3, s[48:49]
	v_mov_b32_e32 v50, v212
	v_mov_b32_e32 v51, v213
	v_xor_b32_e32 v66, 0x80000000, v37
	v_mov_b32_e32 v67, v37
	s_nop 0
	v_pk_mul_f32 v[66:67], v[66:67], v[50:51] op_sel:[0,1] op_sel_hi:[1,0]
	s_nop 0
	v_pk_fma_f32 v[36:37], v[36:37], v[50:51], v[66:67] op_sel_hi:[0,1,1]
	v_add_u32_e32 v50, 0x1200, v16
	v_ashrrev_i32_e32 v51, 31, v50
	v_lshl_add_u64 v[50:51], v[50:51], 3, s[48:49]
	v_mov_b32_e32 v50, v214
	v_mov_b32_e32 v51, v215
	v_xor_b32_e32 v66, 0x80000000, v41
	v_mov_b32_e32 v67, v41
	v_pk_add_f32 v[70:71], v[20:21], v[36:37]
	v_pk_add_f32 v[20:21], v[20:21], v[36:37] neg_lo:[0,1] neg_hi:[0,1]
	s_nop 0
	v_pk_mul_f32 v[66:67], v[66:67], v[50:51] op_sel:[0,1] op_sel_hi:[1,0]
	s_nop 0
	v_pk_fma_f32 v[40:41], v[40:41], v[50:51], v[66:67] op_sel_hi:[0,1,1]
	v_add_u32_e32 v50, 0x1400, v16
	v_ashrrev_i32_e32 v51, 31, v50
	v_lshl_add_u64 v[50:51], v[50:51], 3, s[48:49]
	v_mov_b32_e32 v50, v216
	v_mov_b32_e32 v51, v217
	v_xor_b32_e32 v66, 0x80000000, v43
	v_mov_b32_e32 v67, v43
	v_pk_add_f32 v[36:37], v[22:23], v[40:41]
	v_pk_add_f32 v[22:23], v[22:23], v[40:41] neg_lo:[0,1] neg_hi:[0,1]
	s_nop 0
	v_pk_mul_f32 v[66:67], v[66:67], v[50:51] op_sel:[0,1] op_sel_hi:[1,0]
	s_nop 0
	v_pk_fma_f32 v[42:43], v[42:43], v[50:51], v[66:67] op_sel_hi:[0,1,1]
	v_add_u32_e32 v50, 0x1600, v16
	v_ashrrev_i32_e32 v51, 31, v50
	v_lshl_add_u64 v[50:51], v[50:51], 3, s[48:49]
	v_mov_b32_e32 v50, v218
	v_mov_b32_e32 v51, v219
	v_xor_b32_e32 v66, 0x80000000, v47
	v_mov_b32_e32 v67, v47
	v_xor_b32_e32 v40, 0x80000000, v23
	v_mov_b32_e32 v41, v22
	s_nop 0
	v_pk_mul_f32 v[66:67], v[66:67], v[50:51] op_sel:[0,1] op_sel_hi:[1,0]
	s_nop 0
	v_pk_fma_f32 v[46:47], v[46:47], v[50:51], v[66:67] op_sel_hi:[0,1,1]
	v_add_u32_e32 v50, 0x1800, v16
	v_ashrrev_i32_e32 v51, 31, v50
	v_lshl_add_u64 v[50:51], v[50:51], 3, s[48:49]
	v_mov_b32_e32 v50, v220
	v_mov_b32_e32 v51, v221
	v_xor_b32_e32 v66, 0x80000000, v45
	v_mov_b32_e32 v67, v45
	s_nop 0
	v_pk_mul_f32 v[66:67], v[66:67], v[50:51] op_sel:[0,1] op_sel_hi:[1,0]
	s_nop 0
	v_pk_fma_f32 v[44:45], v[44:45], v[50:51], v[66:67] op_sel_hi:[0,1,1]
	v_add_u32_e32 v50, 0x1a00, v16
	v_ashrrev_i32_e32 v51, 31, v50
	v_lshl_add_u64 v[50:51], v[50:51], 3, s[48:49]
	v_mov_b32_e32 v50, v222
	v_mov_b32_e32 v51, v223
	v_xor_b32_e32 v66, 0x80000000, v49
	v_mov_b32_e32 v67, v49
	s_nop 0
	v_pk_mul_f32 v[66:67], v[66:67], v[50:51] op_sel:[0,1] op_sel_hi:[1,0]
	s_nop 0
	v_pk_fma_f32 v[48:49], v[48:49], v[50:51], v[66:67] op_sel_hi:[0,1,1]
	v_add_u32_e32 v50, 0x1c00, v16
	v_ashrrev_i32_e32 v51, 31, v50
	v_lshl_add_u64 v[50:51], v[50:51], 3, s[48:49]
	v_mov_b32_e32 v50, v224
	v_mov_b32_e32 v51, v225
	v_xor_b32_e32 v66, 0x80000000, v39
	v_mov_b32_e32 v67, v39
	s_nop 0
	v_pk_mul_f32 v[66:67], v[66:67], v[50:51] op_sel:[0,1] op_sel_hi:[1,0]
	s_nop 0
	v_pk_fma_f32 v[38:39], v[38:39], v[50:51], v[66:67] op_sel_hi:[0,1,1]
	v_add_u32_e32 v50, 0x1e00, v16
	v_ashrrev_i32_e32 v51, 31, v50
	v_lshl_add_u64 v[50:51], v[50:51], 3, s[48:49]
	v_mov_b32_e32 v50, v226
	v_mov_b32_e32 v51, v227
	v_lshlrev_b32_e32 v190, 3, v16
	v_add_u32_e32 v190, 0x11000, v190
	global_load_dwordx2 v[196:197], v190, s[48:49] offset:-4096
	global_load_dwordx2 v[198:199], v190, s[48:49]
	v_add_u32_e32 v190, 0x2000, v190
	global_load_dwordx2 v[200:201], v190, s[48:49] offset:-4096
	global_load_dwordx2 v[202:203], v190, s[48:49]
	v_add_u32_e32 v190, 0x2000, v190
	global_load_dwordx2 v[204:205], v190, s[48:49] offset:-4096
	global_load_dwordx2 v[206:207], v190, s[48:49]
	v_add_u32_e32 v190, 0x2000, v190
	global_load_dwordx2 v[208:209], v190, s[48:49] offset:-4096
	global_load_dwordx2 v[210:211], v190, s[48:49]
	v_add_u32_e32 v190, 0x2000, v190
	global_load_dwordx2 v[212:213], v190, s[48:49] offset:-4096
	global_load_dwordx2 v[214:215], v190, s[48:49]
	v_add_u32_e32 v190, 0x2000, v190
	global_load_dwordx2 v[216:217], v190, s[48:49] offset:-4096
	global_load_dwordx2 v[218:219], v190, s[48:49]
	v_add_u32_e32 v190, 0x2000, v190
	global_load_dwordx2 v[220:221], v190, s[48:49] offset:-4096
	global_load_dwordx2 v[222:223], v190, s[48:49]
	v_add_u32_e32 v190, 0x2000, v190
	global_load_dwordx2 v[224:225], v190, s[48:49] offset:-4096
	global_load_dwordx2 v[226:227], v190, s[48:49]
	v_xor_b32_e32 v66, 0x80000000, v19
	v_mov_b32_e32 v67, v19
	v_mov_b32_e32 v17, v165
	s_nop 0
	v_pk_mul_f32 v[66:67], v[66:67], v[50:51] op_sel:[0,1] op_sel_hi:[1,0]
	s_nop 0
	v_pk_fma_f32 v[18:19], v[18:19], v[50:51], v[66:67] op_sel_hi:[0,1,1]
	v_mov_b32_e32 v50, v166
	v_mov_b32_e32 v17, v167
	v_mov_b32_e32 v66, v168
	v_mov_b32_e32 v17, v169
	s_nop 0
	v_pk_mul_f32 v[40:41], v[40:41], v[68:69] op_sel_hi:[1,0]
	v_mov_b32_e32 v17, v171
	v_pk_fma_f32 v[22:23], v[22:23], v[50:51], v[40:41] op_sel_hi:[1,0,1]
	v_pk_add_f32 v[40:41], v[24:25], v[42:43]
	v_pk_add_f32 v[24:25], v[24:25], v[42:43] neg_lo:[0,1] neg_hi:[0,1]
	s_nop 0
	v_xor_b32_e32 v42, 0x80000000, v25
	v_mov_b32_e32 v43, v24
	v_pk_mul_f32 v[42:43], v[42:43], v[66:67] op_sel_hi:[1,0]
	v_mov_b32_e32 v17, v172
	v_pk_fma_f32 v[24:25], v[24:25], v[66:67], v[42:43] op_sel_hi:[1,0,1]
	v_pk_add_f32 v[42:43], v[26:27], v[46:47]
	v_pk_add_f32 v[26:27], v[26:27], v[46:47] neg_lo:[0,1] neg_hi:[0,1]
	s_nop 0
	v_pk_mul_f32 v[46:47], v[26:27], v[68:69] op_sel_hi:[1,0]
	v_xor_b32_e32 v72, 0x80000000, v27
	v_mov_b32_e32 v73, v26
	v_pk_fma_f32 v[26:27], v[72:73], v[50:51], v[46:47] op_sel_hi:[1,0,1]
	v_pk_add_f32 v[46:47], v[28:29], v[44:45]
	v_pk_add_f32 v[28:29], v[28:29], v[44:45] neg_lo:[0,1] neg_hi:[0,1]
	v_mov_b32_e32 v17, v177
	v_xor_b32_e32 v44, 0x80000000, v29
	v_mov_b32_e32 v45, v28
	v_pk_add_f32 v[28:29], v[30:31], v[48:49]
	v_pk_add_f32 v[30:31], v[30:31], v[48:49] neg_lo:[0,1] neg_hi:[0,1]
	s_nop 0
	v_pk_mul_f32 v[48:49], v[30:31], v[68:69] op_sel_hi:[1,0] neg_lo:[0,1] neg_hi:[0,1]
	v_xor_b32_e32 v72, 0x80000000, v31
	v_mov_b32_e32 v73, v30
	v_pk_fma_f32 v[30:31], v[72:73], v[50:51], v[48:49] op_sel_hi:[1,0,1]
	v_pk_add_f32 v[48:49], v[32:33], v[38:39]
	v_pk_add_f32 v[32:33], v[32:33], v[38:39] neg_lo:[0,1] neg_hi:[0,1]
	s_nop 0
	v_xor_b32_e32 v38, 0x80000000, v33
	v_mov_b32_e32 v39, v32
	v_pk_mul_f32 v[38:39], v[38:39], v[66:67] op_sel_hi:[1,0]
	s_nop 0
	v_pk_fma_f32 v[32:33], v[32:33], v[66:67], v[38:39] op_sel_hi:[1,0,1] neg_lo:[0,1,0] neg_hi:[0,1,0]
	v_pk_add_f32 v[38:39], v[34:35], v[18:19]
	v_pk_add_f32 v[18:19], v[34:35], v[18:19] neg_lo:[0,1] neg_hi:[0,1]
	s_nop 0
	v_xor_b32_e32 v34, 0x80000000, v19
	v_mov_b32_e32 v35, v18
	v_pk_mul_f32 v[34:35], v[34:35], v[68:69] op_sel_hi:[1,0]
	v_mov_b32_e32 v68, v170
	v_pk_fma_f32 v[18:19], v[18:19], v[50:51], v[34:35] op_sel_hi:[1,0,1] neg_lo:[0,1,0] neg_hi:[0,1,0]
	v_pk_add_f32 v[50:51], v[36:37], v[28:29]
	v_pk_add_f32 v[28:29], v[36:37], v[28:29] neg_lo:[0,1] neg_hi:[0,1]
	v_pk_add_f32 v[34:35], v[70:71], v[46:47]
	v_xor_b32_e32 v36, 0x80000000, v29
	v_mov_b32_e32 v37, v28
	v_pk_mul_f32 v[36:37], v[36:37], v[66:67] op_sel_hi:[1,0]
	v_pk_add_f32 v[46:47], v[70:71], v[46:47] neg_lo:[0,1] neg_hi:[0,1]
	v_pk_fma_f32 v[28:29], v[28:29], v[66:67], v[36:37] op_sel_hi:[1,0,1]
	v_pk_add_f32 v[36:37], v[40:41], v[48:49]
	v_pk_add_f32 v[40:41], v[40:41], v[48:49] neg_lo:[0,1] neg_hi:[0,1]
	s_nop 0
	v_xor_b32_e32 v48, 0x80000000, v41
	v_mov_b32_e32 v49, v40
	v_pk_add_f32 v[40:41], v[42:43], v[38:39]
	v_pk_add_f32 v[38:39], v[42:43], v[38:39] neg_lo:[0,1] neg_hi:[0,1]
	s_nop 0
	v_xor_b32_e32 v42, 0x80000000, v39
	v_mov_b32_e32 v43, v38
	v_pk_mul_f32 v[42:43], v[66:67], v[42:43] op_sel_hi:[0,1]
	v_pk_fma_f32 v[38:39], v[38:39], v[66:67], v[42:43] op_sel_hi:[1,0,1] neg_lo:[0,1,0] neg_hi:[0,1,0]
	v_pk_add_f32 v[42:43], v[34:35], v[36:37]
	v_pk_add_f32 v[34:35], v[34:35], v[36:37] neg_lo:[0,1] neg_hi:[0,1]
	v_pk_add_f32 v[36:37], v[50:51], v[40:41]
	v_pk_add_f32 v[40:41], v[50:51], v[40:41] neg_lo:[0,1] neg_hi:[0,1]
	s_nop 0
	v_xor_b32_e32 v50, 0x80000000, v41
	v_mov_b32_e32 v51, v40
	v_pk_add_f32 v[40:41], v[42:43], v[36:37]
	v_pk_add_f32 v[36:37], v[42:43], v[36:37] neg_lo:[0,1] neg_hi:[0,1]
	v_pk_add_f32 v[42:43], v[34:35], v[50:51]
	v_pk_add_f32 v[34:35], v[34:35], v[50:51] neg_lo:[0,1] neg_hi:[0,1]
	v_pk_add_f32 v[50:51], v[46:47], v[48:49]
	v_pk_add_f32 v[46:47], v[46:47], v[48:49] neg_lo:[0,1] neg_hi:[0,1]
	v_pk_add_f32 v[48:49], v[28:29], v[38:39]
	v_pk_add_f32 v[28:29], v[28:29], v[38:39] neg_lo:[0,1] neg_hi:[0,1]
	s_nop 0
	v_xor_b32_e32 v38, 0x80000000, v29
	v_mov_b32_e32 v39, v28
	v_pk_add_f32 v[28:29], v[50:51], v[48:49]
	v_pk_add_f32 v[48:49], v[50:51], v[48:49] neg_lo:[0,1] neg_hi:[0,1]
	v_pk_add_f32 v[50:51], v[46:47], v[38:39]
	v_pk_add_f32 v[38:39], v[46:47], v[38:39] neg_lo:[0,1] neg_hi:[0,1]
	v_pk_add_f32 v[46:47], v[20:21], v[44:45]
	v_pk_add_f32 v[20:21], v[20:21], v[44:45] neg_lo:[0,1] neg_hi:[0,1]
	v_pk_add_f32 v[44:45], v[22:23], v[30:31]
	v_pk_add_f32 v[22:23], v[22:23], v[30:31] neg_lo:[0,1] neg_hi:[0,1]
	s_nop 0
	v_xor_b32_e32 v30, 0x80000000, v23
	v_mov_b32_e32 v31, v22
	v_pk_mul_f32 v[30:31], v[66:67], v[30:31] op_sel_hi:[0,1]
	v_pk_fma_f32 v[22:23], v[66:67], v[22:23], v[30:31] op_sel_hi:[0,1,1]
	v_pk_add_f32 v[30:31], v[24:25], v[32:33]
	v_pk_add_f32 v[24:25], v[24:25], v[32:33] neg_lo:[0,1] neg_hi:[0,1]
	s_nop 0
	v_xor_b32_e32 v32, 0x80000000, v25
	v_mov_b32_e32 v33, v24
	v_pk_add_f32 v[24:25], v[26:27], v[18:19]
	v_pk_add_f32 v[18:19], v[26:27], v[18:19] neg_lo:[0,1] neg_hi:[0,1]
	s_nop 0
	v_xor_b32_e32 v26, 0x80000000, v19
	v_mov_b32_e32 v27, v18
	v_pk_mul_f32 v[26:27], v[66:67], v[26:27] op_sel_hi:[0,1]
	v_pk_fma_f32 v[18:19], v[66:67], v[18:19], v[26:27] op_sel_hi:[0,1,1] neg_lo:[1,0,0] neg_hi:[1,0,0]
	v_pk_add_f32 v[26:27], v[46:47], v[30:31]
	v_pk_add_f32 v[30:31], v[46:47], v[30:31] neg_lo:[0,1] neg_hi:[0,1]
	v_pk_add_f32 v[46:47], v[44:45], v[24:25]
	v_pk_add_f32 v[24:25], v[44:45], v[24:25] neg_lo:[0,1] neg_hi:[0,1]
	v_mov_b32_e32 v66, v168
	v_xor_b32_e32 v44, 0x80000000, v25
	v_mov_b32_e32 v45, v24
	v_pk_add_f32 v[24:25], v[26:27], v[46:47]
	v_pk_add_f32 v[26:27], v[26:27], v[46:47] neg_lo:[0,1] neg_hi:[0,1]
	v_pk_add_f32 v[46:47], v[30:31], v[44:45]
	v_pk_add_f32 v[30:31], v[30:31], v[44:45] neg_lo:[0,1] neg_hi:[0,1]
	v_pk_add_f32 v[44:45], v[20:21], v[32:33]
	v_pk_add_f32 v[20:21], v[20:21], v[32:33] neg_lo:[0,1] neg_hi:[0,1]
	v_pk_add_f32 v[32:33], v[22:23], v[18:19]
	v_pk_add_f32 v[18:19], v[22:23], v[18:19] neg_lo:[0,1] neg_hi:[0,1]
	s_nop 0
	v_xor_b32_e32 v22, 0x80000000, v19
	v_mov_b32_e32 v23, v18
	v_pk_add_f32 v[18:19], v[44:45], v[32:33]
	v_pk_add_f32 v[32:33], v[44:45], v[32:33] neg_lo:[0,1] neg_hi:[0,1]
	v_pk_add_f32 v[44:45], v[20:21], v[22:23]
	v_pk_add_f32 v[20:21], v[20:21], v[22:23] neg_lo:[0,1] neg_hi:[0,1]
	ds_write_b64 v10, v[40:41]
	ds_write_b64 v13, v[24:25]
	ds_write_b64 v15, v[28:29]
	ds_write_b64 v52, v[18:19]
	ds_write_b64 v53, v[42:43]
	ds_write_b64 v54, v[46:47]
	ds_write_b64 v55, v[50:51]
	ds_write_b64 v56, v[44:45]
	ds_write_b64 v57, v[36:37]
	ds_write_b64 v58, v[26:27]
	ds_write_b64 v59, v[48:49]
	ds_write_b64 v60, v[32:33]
	ds_write_b64 v61, v[34:35]
	ds_write_b64 v62, v[30:31]
	ds_write_b64 v63, v[38:39]
	ds_write_b64 v64, v[20:21]
	v_mov_b32_e32 v10, v179
	v_mov_b32_e32 v64, v166
	v_lshlrev_b32_e32 v13, 3, v17
	v_lshlrev_b32_e32 v48, 3, v10
	v_add3_u32 v10, 0, v13, v48
	v_xor_b32_e32 v13, 1, v17
	v_xor_b32_e32 v34, 8, v17
	v_xor_b32_e32 v36, 9, v17
	v_lshlrev_b32_e32 v13, 3, v13
	v_xor_b32_e32 v15, 2, v17
	v_xor_b32_e32 v24, 3, v17
	v_xor_b32_e32 v26, 4, v17
	v_xor_b32_e32 v28, 5, v17
	v_xor_b32_e32 v30, 6, v17
	v_xor_b32_e32 v32, 7, v17
	v_lshlrev_b32_e32 v34, 3, v34
	v_lshlrev_b32_e32 v36, 3, v36
	v_xor_b32_e32 v38, 10, v17
	v_xor_b32_e32 v40, 11, v17
	v_xor_b32_e32 v42, 12, v17
	v_xor_b32_e32 v44, 13, v17
	v_xor_b32_e32 v46, 14, v17
	v_xor_b32_e32 v17, 15, v17
	v_add3_u32 v13, 0, v13, v48
	v_lshlrev_b32_e32 v15, 3, v15
	v_lshlrev_b32_e32 v24, 3, v24
	v_lshlrev_b32_e32 v26, 3, v26
	v_lshlrev_b32_e32 v28, 3, v28
	v_lshlrev_b32_e32 v30, 3, v30
	v_lshlrev_b32_e32 v32, 3, v32
	v_add3_u32 v55, 0, v34, v48
	v_add3_u32 v56, 0, v36, v48
	v_lshlrev_b32_e32 v38, 3, v38
	v_lshlrev_b32_e32 v40, 3, v40
	v_lshlrev_b32_e32 v42, 3, v42
	v_lshlrev_b32_e32 v44, 3, v44
	v_lshlrev_b32_e32 v46, 3, v46
	v_lshlrev_b32_e32 v17, 3, v17
	ds_read_b64 v[18:19], v10
	ds_read_b64 v[20:21], v13
	v_add3_u32 v15, 0, v15, v48
	v_add3_u32 v50, 0, v24, v48
	v_add3_u32 v51, 0, v26, v48
	v_add3_u32 v52, 0, v28, v48
	v_add3_u32 v53, 0, v30, v48
	v_add3_u32 v54, 0, v32, v48
	ds_read_b64 v[34:35], v55
	ds_read_b64 v[36:37], v56
	v_add3_u32 v57, 0, v38, v48
	v_add3_u32 v58, 0, v40, v48
	v_add3_u32 v59, 0, v42, v48
	v_add3_u32 v60, 0, v44, v48
	v_add3_u32 v61, 0, v46, v48
	v_add3_u32 v62, 0, v17, v48
	v_mov_b32_e32 v17, v164
	ds_read_b64 v[22:23], v15
	ds_read_b64 v[24:25], v50
	ds_read_b64 v[26:27], v51
	ds_read_b64 v[28:29], v52
	ds_read_b64 v[30:31], v53
	ds_read_b64 v[32:33], v54
	ds_read_b64 v[38:39], v57
	ds_read_b64 v[40:41], v58
	ds_read_b64 v[42:43], v59
	ds_read_b64 v[44:45], v60
	ds_read_b64 v[46:47], v61
	ds_read_b64 v[48:49], v62
	s_waitcnt lgkmcnt(13)
	v_pk_add_f32 v[70:71], v[18:19], v[34:35]
	v_mov_b32_e32 v17, v165
	v_pk_add_f32 v[18:19], v[18:19], v[34:35] neg_lo:[0,1] neg_hi:[0,1]
	v_mov_b32_e32 v17, v167
	s_waitcnt lgkmcnt(12)
	v_pk_add_f32 v[34:35], v[20:21], v[36:37]
	v_pk_add_f32 v[20:21], v[20:21], v[36:37] neg_lo:[0,1] neg_hi:[0,1]
	v_mov_b32_e32 v17, v169
	v_xor_b32_e32 v36, 0x80000000, v21
	v_mov_b32_e32 v37, v20
	s_nop 0
	v_pk_mul_f32 v[36:37], v[36:37], v[68:69] op_sel_hi:[1,0] neg_lo:[0,1] neg_hi:[0,1]
	v_mov_b32_e32 v17, v171
	v_pk_fma_f32 v[20:21], v[20:21], v[64:65], v[36:37] op_sel_hi:[1,0,1]
	s_waitcnt lgkmcnt(5)
	v_pk_add_f32 v[36:37], v[22:23], v[38:39]
	v_pk_add_f32 v[22:23], v[22:23], v[38:39] neg_lo:[0,1] neg_hi:[0,1]
	s_nop 0
	v_xor_b32_e32 v38, 0x80000000, v23
	v_mov_b32_e32 v39, v22
	v_pk_mul_f32 v[38:39], v[38:39], v[66:67] op_sel_hi:[1,0] neg_lo:[0,1] neg_hi:[0,1]
	v_mov_b32_e32 v17, v172
	v_pk_fma_f32 v[22:23], v[22:23], v[66:67], v[38:39] op_sel_hi:[1,0,1]
	s_waitcnt lgkmcnt(4)
	v_pk_add_f32 v[38:39], v[24:25], v[40:41]
	v_pk_add_f32 v[24:25], v[24:25], v[40:41] neg_lo:[0,1] neg_hi:[0,1]
	s_nop 0
	v_pk_mul_f32 v[40:41], v[24:25], v[68:69] op_sel_hi:[1,0]
	v_xor_b32_e32 v72, 0x80000000, v25
	v_mov_b32_e32 v73, v24
	v_pk_fma_f32 v[24:25], v[72:73], v[64:65], v[40:41] op_sel_hi:[1,0,1] neg_lo:[0,1,0] neg_hi:[0,1,0]
	s_waitcnt lgkmcnt(3)
	v_pk_add_f32 v[40:41], v[26:27], v[42:43]
	v_pk_add_f32 v[26:27], v[26:27], v[42:43] neg_lo:[0,1] neg_hi:[0,1]
	s_nop 0
	v_xor_b32_e32 v73, 0x80000000, v26
	v_mov_b32_e32 v72, v27
	s_waitcnt lgkmcnt(2)
	v_pk_add_f32 v[26:27], v[28:29], v[44:45]
	v_pk_add_f32 v[28:29], v[28:29], v[44:45] neg_lo:[0,1] neg_hi:[0,1]
	s_nop 0
	v_pk_mul_f32 v[42:43], v[28:29], v[68:69] op_sel_hi:[1,0] neg_lo:[0,1] neg_hi:[0,1]
	v_xor_b32_e32 v44, 0x80000000, v29
	v_mov_b32_e32 v45, v28
	v_pk_fma_f32 v[28:29], v[44:45], v[64:65], v[42:43] op_sel_hi:[1,0,1] neg_lo:[0,1,0] neg_hi:[0,1,0]
	s_waitcnt lgkmcnt(1)
	v_pk_add_f32 v[42:43], v[30:31], v[46:47]
	v_pk_add_f32 v[30:31], v[30:31], v[46:47] neg_lo:[0,1] neg_hi:[0,1]
	s_nop 0
	v_xor_b32_e32 v44, 0x80000000, v31
	v_mov_b32_e32 v45, v30
	v_pk_mul_f32 v[44:45], v[44:45], v[66:67] op_sel_hi:[1,0] neg_lo:[0,1] neg_hi:[0,1]
	s_nop 0
	v_pk_fma_f32 v[30:31], v[30:31], v[66:67], v[44:45] op_sel_hi:[1,0,1] neg_lo:[0,1,0] neg_hi:[0,1,0]
	s_waitcnt lgkmcnt(0)
	v_pk_add_f32 v[44:45], v[32:33], v[48:49]
	v_pk_add_f32 v[32:33], v[32:33], v[48:49] neg_lo:[0,1] neg_hi:[0,1]
	v_pk_add_f32 v[48:49], v[34:35], v[26:27]
	v_pk_add_f32 v[26:27], v[34:35], v[26:27] neg_lo:[0,1] neg_hi:[0,1]
	v_xor_b32_e32 v46, 0x80000000, v33
	v_xor_b32_e32 v34, 0x80000000, v27
	v_mov_b32_e32 v35, v26
	v_pk_mul_f32 v[34:35], v[34:35], v[66:67] op_sel_hi:[1,0] neg_lo:[0,1] neg_hi:[0,1]
	v_mov_b32_e32 v47, v32
	v_pk_fma_f32 v[26:27], v[26:27], v[66:67], v[34:35] op_sel_hi:[1,0,1]
	v_pk_add_f32 v[34:35], v[36:37], v[42:43]
	v_pk_add_f32 v[36:37], v[36:37], v[42:43] neg_lo:[0,1] neg_hi:[0,1]
	v_pk_mul_f32 v[46:47], v[46:47], v[68:69] op_sel_hi:[1,0] neg_lo:[0,1] neg_hi:[0,1]
	v_xor_b32_e32 v43, 0x80000000, v36
	v_mov_b32_e32 v42, v37
	v_pk_add_f32 v[36:37], v[38:39], v[44:45]
	v_pk_add_f32 v[38:39], v[38:39], v[44:45] neg_lo:[0,1] neg_hi:[0,1]
	v_pk_fma_f32 v[46:47], v[32:33], v[64:65], v[46:47] op_sel_hi:[1,0,1] neg_lo:[0,1,0] neg_hi:[0,1,0]
	v_xor_b32_e32 v44, 0x80000000, v39
	v_mov_b32_e32 v45, v38
	v_pk_add_f32 v[32:33], v[70:71], v[40:41]
	v_pk_mul_f32 v[44:45], v[44:45], v[66:67] op_sel_hi:[1,0] neg_lo:[0,1] neg_hi:[0,1]
	v_pk_add_f32 v[40:41], v[70:71], v[40:41] neg_lo:[0,1] neg_hi:[0,1]
	v_pk_fma_f32 v[38:39], v[38:39], v[66:67], v[44:45] op_sel_hi:[1,0,1] neg_lo:[0,1,0] neg_hi:[0,1,0]
	v_pk_add_f32 v[44:45], v[32:33], v[34:35]
	v_pk_add_f32 v[32:33], v[32:33], v[34:35] neg_lo:[0,1] neg_hi:[0,1]
	v_pk_add_f32 v[34:35], v[48:49], v[36:37]
	v_pk_add_f32 v[36:37], v[48:49], v[36:37] neg_lo:[0,1] neg_hi:[0,1]
	v_pk_add_f32 v[64:65], v[44:45], v[34:35]
	v_xor_b32_e32 v49, 0x80000000, v36
	v_mov_b32_e32 v48, v37
	v_pk_add_f32 v[36:37], v[44:45], v[34:35] neg_lo:[0,1] neg_hi:[0,1]
	v_pk_add_f32 v[68:69], v[32:33], v[48:49]
	v_pk_add_f32 v[44:45], v[32:33], v[48:49] neg_lo:[0,1] neg_hi:[0,1]
	v_pk_add_f32 v[32:33], v[40:41], v[42:43]
	v_pk_add_f32 v[34:35], v[40:41], v[42:43] neg_lo:[0,1] neg_hi:[0,1]
	v_pk_add_f32 v[40:41], v[26:27], v[38:39]
	v_pk_add_f32 v[26:27], v[26:27], v[38:39] neg_lo:[0,1] neg_hi:[0,1]
	v_pk_add_f32 v[42:43], v[32:33], v[40:41] neg_lo:[0,1] neg_hi:[0,1]
	v_xor_b32_e32 v39, 0x80000000, v26
	v_mov_b32_e32 v38, v27
	v_pk_add_f32 v[26:27], v[32:33], v[40:41]
	v_pk_add_f32 v[40:41], v[20:21], v[28:29]
	v_pk_add_f32 v[20:21], v[20:21], v[28:29] neg_lo:[0,1] neg_hi:[0,1]
	v_pk_add_f32 v[32:33], v[34:35], v[38:39]
	v_xor_b32_e32 v28, 0x80000000, v21
	v_mov_b32_e32 v29, v20
	v_pk_mul_f32 v[28:29], v[66:67], v[28:29] op_sel_hi:[0,1] neg_lo:[1,0] neg_hi:[1,0]
	v_pk_fma_f32 v[20:21], v[66:67], v[20:21], v[28:29] op_sel_hi:[0,1,1]
	v_pk_add_f32 v[28:29], v[22:23], v[30:31]
	v_pk_add_f32 v[22:23], v[22:23], v[30:31] neg_lo:[0,1] neg_hi:[0,1]
	v_pk_add_f32 v[38:39], v[34:35], v[38:39] neg_lo:[0,1] neg_hi:[0,1]
	v_xor_b32_e32 v31, 0x80000000, v22
	v_mov_b32_e32 v30, v23
	v_pk_add_f32 v[22:23], v[24:25], v[46:47]
	v_pk_add_f32 v[24:25], v[24:25], v[46:47] neg_lo:[0,1] neg_hi:[0,1]
	v_pk_add_f32 v[34:35], v[18:19], v[72:73]
	v_xor_b32_e32 v46, 0x80000000, v25
	v_mov_b32_e32 v47, v24
	v_pk_mul_f32 v[46:47], v[66:67], v[46:47] op_sel_hi:[0,1] neg_lo:[1,0] neg_hi:[1,0]
	v_pk_fma_f32 v[24:25], v[66:67], v[24:25], v[46:47] op_sel_hi:[0,1,1] neg_lo:[1,0,0] neg_hi:[1,0,0]
	v_pk_add_f32 v[46:47], v[34:35], v[28:29]
	v_pk_add_f32 v[28:29], v[34:35], v[28:29] neg_lo:[0,1] neg_hi:[0,1]
	v_pk_add_f32 v[34:35], v[40:41], v[22:23]
	v_pk_add_f32 v[22:23], v[40:41], v[22:23] neg_lo:[0,1] neg_hi:[0,1]
	v_pk_add_f32 v[18:19], v[18:19], v[72:73] neg_lo:[0,1] neg_hi:[0,1]
	v_xor_b32_e32 v49, 0x80000000, v22
	v_mov_b32_e32 v48, v23
	v_pk_add_f32 v[66:67], v[28:29], v[48:49]
	v_pk_add_f32 v[48:49], v[28:29], v[48:49] neg_lo:[0,1] neg_hi:[0,1]
	v_pk_add_f32 v[28:29], v[18:19], v[30:31]
	v_pk_add_f32 v[18:19], v[18:19], v[30:31] neg_lo:[0,1] neg_hi:[0,1]
	v_pk_add_f32 v[30:31], v[20:21], v[24:25]
	v_pk_add_f32 v[20:21], v[20:21], v[24:25] neg_lo:[0,1] neg_hi:[0,1]
	v_pk_add_f32 v[22:23], v[46:47], v[34:35]
	v_xor_b32_e32 v25, 0x80000000, v20
	v_add_u32_e32 v20, 0x2000, v16
	v_mov_b32_e32 v24, v21
	v_ashrrev_i32_e32 v21, 31, v20
	v_lshl_add_u64 v[20:21], v[20:21], 3, s[48:49]
	s_waitcnt vmcnt(0)
	v_mov_b32_e32 v20, v196
	v_mov_b32_e32 v21, v197
	v_pk_add_f32 v[40:41], v[46:47], v[34:35] neg_lo:[0,1] neg_hi:[0,1]
	v_pk_add_f32 v[34:35], v[18:19], v[24:25]
	v_pk_add_f32 v[18:19], v[18:19], v[24:25] neg_lo:[0,1] neg_hi:[0,1]
	v_xor_b32_e32 v24, 0x80000000, v65
	v_mov_b32_e32 v25, v65
	v_pk_add_f32 v[70:71], v[28:29], v[30:31]
	v_pk_add_f32 v[46:47], v[28:29], v[30:31] neg_lo:[0,1] neg_hi:[0,1]
	v_xor_b32_e32 v28, 0x80000000, v23
	v_mov_b32_e32 v29, v23
	v_xor_b32_e32 v30, 0x80000000, v69
	v_mov_b32_e32 v31, v69
	s_nop 0
	v_pk_mul_f32 v[24:25], v[24:25], v[20:21] op_sel:[0,1] op_sel_hi:[1,0]
	s_nop 0
	v_pk_fma_f32 v[20:21], v[64:65], v[20:21], v[24:25] op_sel_hi:[0,1,1]
	v_add_u32_e32 v24, 0x2200, v16
	v_ashrrev_i32_e32 v25, 31, v24
	v_lshl_add_u64 v[24:25], v[24:25], 3, s[48:49]
	v_mov_b32_e32 v24, v198
	v_mov_b32_e32 v25, v199
	v_xor_b32_e32 v64, 0x80000000, v67
	v_mov_b32_e32 v65, v67
	s_nop 0
	v_pk_mul_f32 v[28:29], v[24:25], v[28:29] op_sel:[1,0] op_sel_hi:[0,1]
	v_pk_fma_f32 v[22:23], v[24:25], v[22:23], v[28:29] op_sel_hi:[1,0,1]
	v_add_u32_e32 v24, 0x2400, v16
	v_ashrrev_i32_e32 v25, 31, v24
	v_lshl_add_u64 v[24:25], v[24:25], 3, s[48:49]
	v_mov_b32_e32 v24, v200
	v_mov_b32_e32 v25, v201
	v_xor_b32_e32 v28, 0x80000000, v27
	v_mov_b32_e32 v29, v27
	s_nop 0
	v_pk_mul_f32 v[28:29], v[28:29], v[24:25] op_sel:[0,1] op_sel_hi:[1,0]
	s_nop 0
	v_pk_fma_f32 v[24:25], v[26:27], v[24:25], v[28:29] op_sel_hi:[0,1,1]
	v_add_u32_e32 v26, 0x2600, v16
	v_ashrrev_i32_e32 v27, 31, v26
	v_lshl_add_u64 v[26:27], v[26:27], 3, s[48:49]
	v_mov_b32_e32 v26, v202
	v_mov_b32_e32 v27, v203
	v_xor_b32_e32 v28, 0x80000000, v71
	v_mov_b32_e32 v29, v71
	s_nop 0
	v_pk_mul_f32 v[28:29], v[26:27], v[28:29] op_sel:[1,0] op_sel_hi:[0,1]
	v_pk_fma_f32 v[26:27], v[26:27], v[70:71], v[28:29] op_sel_hi:[1,0,1]
	v_add_u32_e32 v28, 0x2800, v16
	v_ashrrev_i32_e32 v29, 31, v28
	v_lshl_add_u64 v[28:29], v[28:29], 3, s[48:49]
	v_mov_b32_e32 v28, v204
	v_mov_b32_e32 v29, v205
	s_nop 0
	v_pk_mul_f32 v[30:31], v[30:31], v[28:29] op_sel:[0,1] op_sel_hi:[1,0]
	s_nop 0
	v_pk_fma_f32 v[28:29], v[68:69], v[28:29], v[30:31] op_sel_hi:[0,1,1]
	v_add_u32_e32 v30, 0x2a00, v16
	v_ashrrev_i32_e32 v31, 31, v30
	v_lshl_add_u64 v[30:31], v[30:31], 3, s[48:49]
	v_mov_b32_e32 v30, v206
	v_mov_b32_e32 v31, v207
	s_nop 0
	v_pk_mul_f32 v[64:65], v[30:31], v[64:65] op_sel:[1,0] op_sel_hi:[0,1]
	v_pk_fma_f32 v[30:31], v[30:31], v[66:67], v[64:65] op_sel_hi:[1,0,1]
	v_add_u32_e32 v64, 0x2c00, v16
	v_ashrrev_i32_e32 v65, 31, v64
	v_lshl_add_u64 v[64:65], v[64:65], 3, s[48:49]
	v_mov_b32_e32 v64, v208
	v_mov_b32_e32 v65, v209
	v_xor_b32_e32 v66, 0x80000000, v33
	v_mov_b32_e32 v67, v33
	s_nop 0
	v_pk_mul_f32 v[66:67], v[66:67], v[64:65] op_sel:[0,1] op_sel_hi:[1,0]
	s_nop 0
	v_pk_fma_f32 v[32:33], v[32:33], v[64:65], v[66:67] op_sel_hi:[0,1,1]
	v_add_u32_e32 v64, 0x2e00, v16
	v_ashrrev_i32_e32 v65, 31, v64
	v_lshl_add_u64 v[64:65], v[64:65], 3, s[48:49]
	v_mov_b32_e32 v64, v210
	v_mov_b32_e32 v65, v211
	v_xor_b32_e32 v66, 0x80000000, v35
	v_mov_b32_e32 v67, v35
	s_nop 0
	v_pk_mul_f32 v[66:67], v[64:65], v[66:67] op_sel:[1,0] op_sel_hi:[0,1]
	v_pk_fma_f32 v[34:35], v[64:65], v[34:35], v[66:67] op_sel_hi:[1,0,1]
	v_add_u32_e32 v64, 0x3000, v16
	v_ashrrev_i32_e32 v65, 31, v64
	v_lshl_add_u64 v[64:65], v[64:65], 3, s[48:49]
	v_mov_b32_e32 v64, v212
	v_mov_b32_e32 v65, v213
	v_xor_b32_e32 v66, 0x80000000, v37
	v_mov_b32_e32 v67, v37
	s_nop 0
	v_pk_mul_f32 v[66:67], v[66:67], v[64:65] op_sel:[0,1] op_sel_hi:[1,0]
	s_nop 0
	v_pk_fma_f32 v[36:37], v[36:37], v[64:65], v[66:67] op_sel_hi:[0,1,1]
	v_add_u32_e32 v64, 0x3200, v16
	v_ashrrev_i32_e32 v65, 31, v64
	v_lshl_add_u64 v[64:65], v[64:65], 3, s[48:49]
	v_mov_b32_e32 v64, v214
	v_mov_b32_e32 v65, v215
	v_xor_b32_e32 v66, 0x80000000, v41
	v_mov_b32_e32 v67, v41
	v_pk_add_f32 v[68:69], v[20:21], v[36:37]
	v_pk_add_f32 v[20:21], v[20:21], v[36:37] neg_lo:[0,1] neg_hi:[0,1]
	s_nop 0
	v_pk_mul_f32 v[66:67], v[66:67], v[64:65] op_sel:[0,1] op_sel_hi:[1,0]
	s_nop 0
	v_pk_fma_f32 v[40:41], v[40:41], v[64:65], v[66:67] op_sel_hi:[0,1,1]
	v_add_u32_e32 v64, 0x3400, v16
	v_ashrrev_i32_e32 v65, 31, v64
	v_lshl_add_u64 v[64:65], v[64:65], 3, s[48:49]
	v_mov_b32_e32 v64, v216
	v_mov_b32_e32 v65, v217
	v_xor_b32_e32 v66, 0x80000000, v43
	v_mov_b32_e32 v67, v43
	v_pk_add_f32 v[36:37], v[22:23], v[40:41]
	v_pk_add_f32 v[22:23], v[22:23], v[40:41] neg_lo:[0,1] neg_hi:[0,1]
	s_nop 0
	v_pk_mul_f32 v[66:67], v[66:67], v[64:65] op_sel:[0,1] op_sel_hi:[1,0]
	s_nop 0
	v_pk_fma_f32 v[42:43], v[42:43], v[64:65], v[66:67] op_sel_hi:[0,1,1]
	v_add_u32_e32 v64, 0x3600, v16
	v_ashrrev_i32_e32 v65, 31, v64
	v_lshl_add_u64 v[64:65], v[64:65], 3, s[48:49]
	v_mov_b32_e32 v64, v218
	v_mov_b32_e32 v65, v219
	v_xor_b32_e32 v66, 0x80000000, v47
	v_mov_b32_e32 v67, v47
	v_xor_b32_e32 v40, 0x80000000, v23
	v_mov_b32_e32 v41, v22
	s_nop 0
	v_pk_mul_f32 v[66:67], v[66:67], v[64:65] op_sel:[0,1] op_sel_hi:[1,0]
	s_nop 0
	v_pk_fma_f32 v[46:47], v[46:47], v[64:65], v[66:67] op_sel_hi:[0,1,1]
	v_add_u32_e32 v64, 0x3800, v16
	v_ashrrev_i32_e32 v65, 31, v64
	v_lshl_add_u64 v[64:65], v[64:65], 3, s[48:49]
	v_mov_b32_e32 v64, v220
	v_mov_b32_e32 v65, v221
	v_xor_b32_e32 v66, 0x80000000, v45
	v_mov_b32_e32 v67, v45
	s_nop 0
	v_pk_mul_f32 v[66:67], v[66:67], v[64:65] op_sel:[0,1] op_sel_hi:[1,0]
	s_nop 0
	v_pk_fma_f32 v[44:45], v[44:45], v[64:65], v[66:67] op_sel_hi:[0,1,1]
	v_add_u32_e32 v64, 0x3a00, v16
	v_ashrrev_i32_e32 v65, 31, v64
	v_lshl_add_u64 v[64:65], v[64:65], 3, s[48:49]
	v_mov_b32_e32 v64, v222
	v_mov_b32_e32 v65, v223
	v_xor_b32_e32 v66, 0x80000000, v49
	v_mov_b32_e32 v67, v49
	s_nop 0
	v_pk_mul_f32 v[66:67], v[66:67], v[64:65] op_sel:[0,1] op_sel_hi:[1,0]
	s_nop 0
	v_pk_fma_f32 v[48:49], v[48:49], v[64:65], v[66:67] op_sel_hi:[0,1,1]
	v_add_u32_e32 v64, 0x3c00, v16
	v_ashrrev_i32_e32 v65, 31, v64
	v_lshl_add_u64 v[64:65], v[64:65], 3, s[48:49]
	v_add_u32_e32 v16, 0x3e00, v16
	v_mov_b32_e32 v64, v224
	v_mov_b32_e32 v65, v225
	v_ashrrev_i32_e32 v17, 31, v16
	v_lshl_add_u64 v[16:17], v[16:17], 3, s[48:49]
	v_mov_b32_e32 v16, v226
	v_mov_b32_e32 v17, v227
	v_xor_b32_e32 v66, 0x80000000, v39
	v_mov_b32_e32 v67, v39
	s_nop 0
	v_pk_mul_f32 v[66:67], v[66:67], v[64:65] op_sel:[0,1] op_sel_hi:[1,0]
	s_nop 0
	v_pk_fma_f32 v[38:39], v[38:39], v[64:65], v[66:67] op_sel_hi:[0,1,1]
	v_xor_b32_e32 v64, 0x80000000, v19
	v_mov_b32_e32 v65, v19
	s_nop 0
	v_pk_mul_f32 v[64:65], v[64:65], v[16:17] op_sel:[0,1] op_sel_hi:[1,0]
	v_mov_b32_e32 v66, v170
	v_pk_fma_f32 v[16:17], v[18:19], v[16:17], v[64:65] op_sel_hi:[0,1,1]
	v_mov_b32_e32 v18, v164
	v_mov_b32_e32 v19, v167
	v_mov_b32_e32 v18, v165
	v_mov_b32_e32 v64, v168
	v_mov_b32_e32 v18, v166
	s_nop 0
	v_mov_b32_e32 v19, v169
	s_nop 0
	v_mov_b32_e32 v19, v171
	v_pk_mul_f32 v[40:41], v[40:41], v[66:67] op_sel_hi:[1,0]
	v_mov_b32_e32 v19, v172
	s_nop 0
	v_pk_fma_f32 v[22:23], v[22:23], v[18:19], v[40:41] op_sel_hi:[1,0,1]
	v_pk_add_f32 v[40:41], v[24:25], v[42:43]
	v_pk_add_f32 v[24:25], v[24:25], v[42:43] neg_lo:[0,1] neg_hi:[0,1]
	s_nop 0
	v_xor_b32_e32 v42, 0x80000000, v25
	v_mov_b32_e32 v43, v24
	v_pk_mul_f32 v[42:43], v[42:43], v[64:65] op_sel_hi:[1,0]
	s_nop 0
	v_pk_fma_f32 v[24:25], v[24:25], v[64:65], v[42:43] op_sel_hi:[1,0,1]
	v_pk_add_f32 v[42:43], v[26:27], v[46:47]
	v_pk_add_f32 v[26:27], v[26:27], v[46:47] neg_lo:[0,1] neg_hi:[0,1]
	s_nop 0
	v_pk_mul_f32 v[46:47], v[26:27], v[66:67] op_sel_hi:[1,0]
	v_xor_b32_e32 v70, 0x80000000, v27
	v_mov_b32_e32 v71, v26
	v_pk_fma_f32 v[26:27], v[70:71], v[18:19], v[46:47] op_sel_hi:[1,0,1]
	v_pk_add_f32 v[46:47], v[28:29], v[44:45]
	v_pk_add_f32 v[28:29], v[28:29], v[44:45] neg_lo:[0,1] neg_hi:[0,1]
	s_nop 0
	v_xor_b32_e32 v44, 0x80000000, v29
	v_mov_b32_e32 v45, v28
	v_pk_add_f32 v[28:29], v[30:31], v[48:49]
	v_pk_add_f32 v[30:31], v[30:31], v[48:49] neg_lo:[0,1] neg_hi:[0,1]
	s_nop 0
	v_pk_mul_f32 v[48:49], v[30:31], v[66:67] op_sel_hi:[1,0] neg_lo:[0,1] neg_hi:[0,1]
	v_xor_b32_e32 v70, 0x80000000, v31
	v_mov_b32_e32 v71, v30
	v_pk_fma_f32 v[30:31], v[70:71], v[18:19], v[48:49] op_sel_hi:[1,0,1]
	v_pk_add_f32 v[48:49], v[32:33], v[38:39]
	v_pk_add_f32 v[32:33], v[32:33], v[38:39] neg_lo:[0,1] neg_hi:[0,1]
	s_nop 0
	v_xor_b32_e32 v38, 0x80000000, v33
	v_mov_b32_e32 v39, v32
	v_pk_mul_f32 v[38:39], v[38:39], v[64:65] op_sel_hi:[1,0]
	s_nop 0
	v_pk_fma_f32 v[32:33], v[32:33], v[64:65], v[38:39] op_sel_hi:[1,0,1] neg_lo:[0,1,0] neg_hi:[0,1,0]
	v_pk_add_f32 v[38:39], v[34:35], v[16:17]
	v_pk_add_f32 v[16:17], v[34:35], v[16:17] neg_lo:[0,1] neg_hi:[0,1]
	s_nop 0
	v_xor_b32_e32 v34, 0x80000000, v17
	v_mov_b32_e32 v35, v16
	v_pk_mul_f32 v[34:35], v[34:35], v[66:67] op_sel_hi:[1,0]
	s_nop 0
	v_pk_fma_f32 v[16:17], v[16:17], v[18:19], v[34:35] op_sel_hi:[1,0,1] neg_lo:[0,1,0] neg_hi:[0,1,0]
	v_pk_add_f32 v[18:19], v[68:69], v[46:47]
	v_pk_add_f32 v[34:35], v[68:69], v[46:47] neg_lo:[0,1] neg_hi:[0,1]
	v_pk_add_f32 v[46:47], v[36:37], v[28:29]
	v_pk_add_f32 v[28:29], v[36:37], v[28:29] neg_lo:[0,1] neg_hi:[0,1]
	s_nop 0
	v_xor_b32_e32 v36, 0x80000000, v29
	v_mov_b32_e32 v37, v28
	v_pk_mul_f32 v[36:37], v[36:37], v[64:65] op_sel_hi:[1,0]
	s_nop 0
	v_pk_fma_f32 v[28:29], v[28:29], v[64:65], v[36:37] op_sel_hi:[1,0,1]
	v_pk_add_f32 v[36:37], v[40:41], v[48:49]
	v_pk_add_f32 v[40:41], v[40:41], v[48:49] neg_lo:[0,1] neg_hi:[0,1]
	s_nop 0
	v_xor_b32_e32 v48, 0x80000000, v41
	v_mov_b32_e32 v49, v40
	v_pk_add_f32 v[40:41], v[42:43], v[38:39]
	v_pk_add_f32 v[38:39], v[42:43], v[38:39] neg_lo:[0,1] neg_hi:[0,1]
	s_nop 0
	v_xor_b32_e32 v42, 0x80000000, v39
	v_mov_b32_e32 v43, v38
	v_pk_mul_f32 v[42:43], v[64:65], v[42:43] op_sel_hi:[0,1]
	v_pk_fma_f32 v[38:39], v[38:39], v[64:65], v[42:43] op_sel_hi:[1,0,1] neg_lo:[0,1,0] neg_hi:[0,1,0]
	v_pk_add_f32 v[42:43], v[18:19], v[36:37]
	v_pk_add_f32 v[18:19], v[18:19], v[36:37] neg_lo:[0,1] neg_hi:[0,1]
	v_pk_add_f32 v[36:37], v[46:47], v[40:41]
	v_pk_add_f32 v[40:41], v[46:47], v[40:41] neg_lo:[0,1] neg_hi:[0,1]
	s_nop 0
	v_xor_b32_e32 v46, 0x80000000, v41
	v_mov_b32_e32 v47, v40
	v_pk_add_f32 v[40:41], v[42:43], v[36:37]
	v_pk_add_f32 v[36:37], v[42:43], v[36:37] neg_lo:[0,1] neg_hi:[0,1]
	v_pk_add_f32 v[42:43], v[18:19], v[46:47]
	v_pk_add_f32 v[18:19], v[18:19], v[46:47] neg_lo:[0,1] neg_hi:[0,1]
	v_pk_add_f32 v[46:47], v[34:35], v[48:49]
	v_pk_add_f32 v[34:35], v[34:35], v[48:49] neg_lo:[0,1] neg_hi:[0,1]
	v_pk_add_f32 v[48:49], v[28:29], v[38:39]
	v_pk_add_f32 v[28:29], v[28:29], v[38:39] neg_lo:[0,1] neg_hi:[0,1]
	s_nop 0
	v_xor_b32_e32 v38, 0x80000000, v29
	v_mov_b32_e32 v39, v28
	v_pk_add_f32 v[28:29], v[46:47], v[48:49]
	v_pk_add_f32 v[46:47], v[46:47], v[48:49] neg_lo:[0,1] neg_hi:[0,1]
	v_pk_add_f32 v[48:49], v[34:35], v[38:39]
	v_pk_add_f32 v[34:35], v[34:35], v[38:39] neg_lo:[0,1] neg_hi:[0,1]
	v_pk_add_f32 v[38:39], v[20:21], v[44:45]
	v_pk_add_f32 v[20:21], v[20:21], v[44:45] neg_lo:[0,1] neg_hi:[0,1]
	v_pk_add_f32 v[44:45], v[22:23], v[30:31]
	v_pk_add_f32 v[22:23], v[22:23], v[30:31] neg_lo:[0,1] neg_hi:[0,1]
	s_nop 0
	v_xor_b32_e32 v30, 0x80000000, v23
	v_mov_b32_e32 v31, v22
	v_pk_mul_f32 v[30:31], v[64:65], v[30:31] op_sel_hi:[0,1]
	v_pk_fma_f32 v[22:23], v[64:65], v[22:23], v[30:31] op_sel_hi:[0,1,1]
	v_pk_add_f32 v[30:31], v[24:25], v[32:33]
	v_pk_add_f32 v[24:25], v[24:25], v[32:33] neg_lo:[0,1] neg_hi:[0,1]
	s_nop 0
	v_xor_b32_e32 v32, 0x80000000, v25
	v_mov_b32_e32 v33, v24
	v_pk_add_f32 v[24:25], v[26:27], v[16:17]
	v_pk_add_f32 v[16:17], v[26:27], v[16:17] neg_lo:[0,1] neg_hi:[0,1]
	s_nop 0
	v_xor_b32_e32 v26, 0x80000000, v17
	v_mov_b32_e32 v27, v16
	v_pk_mul_f32 v[26:27], v[64:65], v[26:27] op_sel_hi:[0,1]
	v_pk_fma_f32 v[16:17], v[64:65], v[16:17], v[26:27] op_sel_hi:[0,1,1] neg_lo:[1,0,0] neg_hi:[1,0,0]
	v_pk_add_f32 v[26:27], v[38:39], v[30:31]
	v_pk_add_f32 v[30:31], v[38:39], v[30:31] neg_lo:[0,1] neg_hi:[0,1]
	v_pk_add_f32 v[38:39], v[44:45], v[24:25]
	v_pk_add_f32 v[24:25], v[44:45], v[24:25] neg_lo:[0,1] neg_hi:[0,1]
	s_nop 0
	v_xor_b32_e32 v44, 0x80000000, v25
	v_mov_b32_e32 v45, v24
	v_pk_add_f32 v[24:25], v[26:27], v[38:39]
	v_pk_add_f32 v[26:27], v[26:27], v[38:39] neg_lo:[0,1] neg_hi:[0,1]
	v_pk_add_f32 v[38:39], v[30:31], v[44:45]
	v_pk_add_f32 v[30:31], v[30:31], v[44:45] neg_lo:[0,1] neg_hi:[0,1]
	v_pk_add_f32 v[44:45], v[20:21], v[32:33]
	v_pk_add_f32 v[20:21], v[20:21], v[32:33] neg_lo:[0,1] neg_hi:[0,1]
	v_pk_add_f32 v[32:33], v[22:23], v[16:17]
	v_pk_add_f32 v[16:17], v[22:23], v[16:17] neg_lo:[0,1] neg_hi:[0,1]
	s_nop 0
	v_xor_b32_e32 v22, 0x80000000, v17
	v_mov_b32_e32 v23, v16
	v_pk_add_f32 v[16:17], v[44:45], v[32:33]
	v_pk_add_f32 v[32:33], v[44:45], v[32:33] neg_lo:[0,1] neg_hi:[0,1]
	v_pk_add_f32 v[44:45], v[20:21], v[22:23]
	v_pk_add_f32 v[20:21], v[20:21], v[22:23] neg_lo:[0,1] neg_hi:[0,1]
	ds_write_b64 v10, v[40:41]
	ds_write_b64 v13, v[24:25]
	ds_write_b64 v15, v[28:29]
	ds_write_b64 v50, v[16:17]
	ds_write_b64 v51, v[42:43]
	ds_write_b64 v52, v[38:39]
	ds_write_b64 v53, v[48:49]
	ds_write_b64 v54, v[44:45]
	ds_write_b64 v55, v[36:37]
	ds_write_b64 v56, v[26:27]
	ds_write_b64 v57, v[46:47]
	ds_write_b64 v58, v[32:33]
	ds_write_b64 v59, v[18:19]
	ds_write_b64 v60, v[30:31]
	ds_write_b64 v61, v[34:35]
	ds_write_b64 v62, v[20:21]
	v_mov_b32_e32 v10, v176
	v_mov_b32_e32 v50, v173
	s_waitcnt lgkmcnt(0)
	s_barrier
	v_mov_b32_e32 v20, v182
	v_add_u32_e32 v13, v50, v10
	v_mov_b32_e32 v21, v183
	v_lshl_add_u32 v13, v13, 3, 0
	ds_read2_b64 v[16:19], v13 offset1:16
	v_xad_u32 v15, v50, 1, v10
	v_lshl_add_u32 v15, v15, 3, 0
	s_waitcnt lgkmcnt(0)
	v_xor_b32_e32 v23, 0x80000000, v16
	v_mov_b32_e32 v22, v17
	v_pk_fma_f32 v[16:17], v[22:23], 0, v[16:17] op_sel_hi:[1,0,1]
	v_pk_fma_f32 v[22:23], v[20:21], s[92:93], v[20:21] op_sel:[1,0,0] op_sel_hi:[0,1,1]
	v_xor_b32_e32 v25, 0x80000000, v18
	v_mov_b32_e32 v24, v19
	v_pk_mul_f32 v[24:25], v[22:23], v[24:25] op_sel:[1,0]
	s_nop 0
	v_pk_fma_f32 v[18:19], v[18:19], v[22:23], v[24:25] op_sel_hi:[1,0,1]
	v_xor_b32_e32 v24, 0x80000000, v23
	v_mov_b32_e32 v25, v23
	v_pk_mul_f32 v[24:25], v[20:21], v[24:25] op_sel:[1,0] op_sel_hi:[0,1]
	v_pk_fma_f32 v[26:27], v[20:21], v[22:23], v[24:25] op_sel_hi:[1,0,1]
	ds_read2_b64 v[22:25], v15 offset0:32 offset1:48
	s_waitcnt lgkmcnt(0)
	v_xor_b32_e32 v29, 0x80000000, v22
	v_mov_b32_e32 v28, v23
	v_pk_mul_f32 v[28:29], v[28:29], v[26:27] op_sel:[0,1]
	s_nop 0
	v_pk_fma_f32 v[22:23], v[22:23], v[26:27], v[28:29] op_sel_hi:[1,0,1]
	v_xor_b32_e32 v28, 0x80000000, v27
	v_mov_b32_e32 v29, v27
	v_pk_mul_f32 v[28:29], v[20:21], v[28:29] op_sel:[1,0] op_sel_hi:[0,1]
	v_pk_fma_f32 v[26:27], v[20:21], v[26:27], v[28:29] op_sel_hi:[1,0,1]
	v_xor_b32_e32 v29, 0x80000000, v24
	v_mov_b32_e32 v28, v25
	v_pk_mul_f32 v[28:29], v[28:29], v[26:27] op_sel:[0,1]
	s_nop 0
	v_pk_fma_f32 v[24:25], v[24:25], v[26:27], v[28:29] op_sel_hi:[1,0,1]
	v_xor_b32_e32 v28, 0x80000000, v27
	v_mov_b32_e32 v29, v27
	v_pk_mul_f32 v[28:29], v[20:21], v[28:29] op_sel:[1,0] op_sel_hi:[0,1]
	v_pk_fma_f32 v[26:27], v[20:21], v[26:27], v[28:29] op_sel_hi:[1,0,1]
	v_xad_u32 v28, v50, 2, v10
	v_lshl_add_u32 v51, v28, 3, 0
	ds_read2_b64 v[28:31], v51 offset0:64 offset1:80
	v_xor_b32_e32 v32, 0x80000000, v27
	v_mov_b32_e32 v33, v27
	v_pk_mul_f32 v[32:33], v[20:21], v[32:33] op_sel:[1,0] op_sel_hi:[0,1]
	s_waitcnt lgkmcnt(0)
	v_xor_b32_e32 v35, 0x80000000, v28
	v_mov_b32_e32 v34, v29
	v_pk_mul_f32 v[34:35], v[34:35], v[26:27] op_sel:[0,1]
	s_nop 0
	v_pk_fma_f32 v[28:29], v[28:29], v[26:27], v[34:35] op_sel_hi:[1,0,1]
	v_pk_fma_f32 v[34:35], v[20:21], v[26:27], v[32:33] op_sel_hi:[1,0,1]
	v_xor_b32_e32 v27, 0x80000000, v30
	v_mov_b32_e32 v26, v31
	v_pk_mul_f32 v[26:27], v[26:27], v[34:35] op_sel:[0,1]
	v_xor_b32_e32 v36, 0x80000000, v35
	v_pk_fma_f32 v[26:27], v[30:31], v[34:35], v[26:27] op_sel_hi:[1,0,1]
	v_xad_u32 v30, v50, 3, v10
	v_lshl_add_u32 v54, v30, 3, 0
	ds_read2_b64 v[30:33], v54 offset0:96 offset1:112
	v_mov_b32_e32 v37, v35
	v_pk_mul_f32 v[36:37], v[20:21], v[36:37] op_sel:[1,0] op_sel_hi:[0,1]
	v_pk_fma_f32 v[34:35], v[20:21], v[34:35], v[36:37] op_sel_hi:[1,0,1]
	s_waitcnt lgkmcnt(0)
	v_xor_b32_e32 v37, 0x80000000, v30
	v_mov_b32_e32 v36, v31
	v_pk_mul_f32 v[36:37], v[36:37], v[34:35] op_sel:[0,1]
	s_nop 0
	v_pk_fma_f32 v[30:31], v[30:31], v[34:35], v[36:37] op_sel_hi:[1,0,1]
	v_xor_b32_e32 v36, 0x80000000, v35
	v_mov_b32_e32 v37, v35
	v_pk_mul_f32 v[36:37], v[20:21], v[36:37] op_sel:[1,0] op_sel_hi:[0,1]
	v_pk_fma_f32 v[34:35], v[20:21], v[34:35], v[36:37] op_sel_hi:[1,0,1]
	v_xor_b32_e32 v37, 0x80000000, v32
	v_mov_b32_e32 v36, v33
	v_pk_mul_f32 v[36:37], v[36:37], v[34:35] op_sel:[0,1]
	s_nop 0
	v_pk_fma_f32 v[32:33], v[32:33], v[34:35], v[36:37] op_sel_hi:[1,0,1]
	v_xor_b32_e32 v36, 0x80000000, v35
	v_mov_b32_e32 v37, v35
	v_pk_mul_f32 v[36:37], v[20:21], v[36:37] op_sel:[1,0] op_sel_hi:[0,1]
	v_pk_fma_f32 v[38:39], v[20:21], v[34:35], v[36:37] op_sel_hi:[1,0,1]
	v_xad_u32 v34, v50, 4, v10
	v_lshl_add_u32 v55, v34, 3, 0
	ds_read2_b64 v[34:37], v55 offset0:128 offset1:144
	v_xor_b32_e32 v40, 0x80000000, v39
	v_mov_b32_e32 v41, v39
	v_pk_mul_f32 v[40:41], v[20:21], v[40:41] op_sel:[1,0] op_sel_hi:[0,1]
	s_waitcnt lgkmcnt(0)
	v_xor_b32_e32 v43, 0x80000000, v34
	v_mov_b32_e32 v42, v35
	v_pk_mul_f32 v[42:43], v[42:43], v[38:39] op_sel:[0,1]
	s_nop 0
	v_pk_fma_f32 v[34:35], v[34:35], v[38:39], v[42:43] op_sel_hi:[1,0,1]
	v_pk_fma_f32 v[42:43], v[20:21], v[38:39], v[40:41] op_sel_hi:[1,0,1]
	v_xor_b32_e32 v39, 0x80000000, v36
	v_mov_b32_e32 v38, v37
	v_pk_mul_f32 v[38:39], v[38:39], v[42:43] op_sel:[0,1]
	v_xor_b32_e32 v44, 0x80000000, v43
	v_pk_fma_f32 v[36:37], v[36:37], v[42:43], v[38:39] op_sel_hi:[1,0,1]
	v_xad_u32 v38, v50, 5, v10
	v_lshl_add_u32 v56, v38, 3, 0
	ds_read2_b64 v[38:41], v56 offset0:160 offset1:176
	v_mov_b32_e32 v45, v43
	v_pk_mul_f32 v[44:45], v[20:21], v[44:45] op_sel:[1,0] op_sel_hi:[0,1]
	v_pk_fma_f32 v[42:43], v[20:21], v[42:43], v[44:45] op_sel_hi:[1,0,1]
	s_waitcnt lgkmcnt(0)
	v_xor_b32_e32 v45, 0x80000000, v38
	v_mov_b32_e32 v44, v39
	v_pk_mul_f32 v[44:45], v[44:45], v[42:43] op_sel:[0,1]
	s_nop 0
	v_pk_fma_f32 v[38:39], v[38:39], v[42:43], v[44:45] op_sel_hi:[1,0,1]
	v_xor_b32_e32 v44, 0x80000000, v43
	v_mov_b32_e32 v45, v43
	v_pk_mul_f32 v[44:45], v[20:21], v[44:45] op_sel:[1,0] op_sel_hi:[0,1]
	v_pk_fma_f32 v[42:43], v[20:21], v[42:43], v[44:45] op_sel_hi:[1,0,1]
	v_xor_b32_e32 v45, 0x80000000, v40
	v_mov_b32_e32 v44, v41
	v_pk_mul_f32 v[44:45], v[44:45], v[42:43] op_sel:[0,1]
	s_nop 0
	v_pk_fma_f32 v[40:41], v[40:41], v[42:43], v[44:45] op_sel_hi:[1,0,1]
	v_xor_b32_e32 v44, 0x80000000, v43
	v_mov_b32_e32 v45, v43
	v_pk_mul_f32 v[44:45], v[20:21], v[44:45] op_sel:[1,0] op_sel_hi:[0,1]
	v_pk_fma_f32 v[42:43], v[20:21], v[42:43], v[44:45] op_sel_hi:[1,0,1]
	v_xad_u32 v44, v50, 6, v10
	v_lshl_add_u32 v57, v44, 3, 0
	ds_read2_b64 v[44:47], v57 offset0:192 offset1:208
	v_xor_b32_e32 v48, 0x80000000, v43
	v_mov_b32_e32 v49, v43
	v_pk_mul_f32 v[48:49], v[20:21], v[48:49] op_sel:[1,0] op_sel_hi:[0,1]
	s_waitcnt lgkmcnt(0)
	v_xor_b32_e32 v53, 0x80000000, v44
	v_mov_b32_e32 v52, v45
	v_pk_mul_f32 v[52:53], v[52:53], v[42:43] op_sel:[0,1]
	s_nop 0
	v_pk_fma_f32 v[44:45], v[44:45], v[42:43], v[52:53] op_sel_hi:[1,0,1]
	v_pk_fma_f32 v[52:53], v[20:21], v[42:43], v[48:49] op_sel_hi:[1,0,1]
	v_xor_b32_e32 v43, 0x80000000, v46
	v_mov_b32_e32 v42, v47
	v_pk_mul_f32 v[42:43], v[42:43], v[52:53] op_sel:[0,1]
	v_xor_b32_e32 v60, 0x80000000, v53
	v_pk_fma_f32 v[42:43], v[46:47], v[52:53], v[42:43] op_sel_hi:[1,0,1]
	v_xad_u32 v46, v50, 7, v10
	v_lshl_add_u32 v58, v46, 3, 0
	ds_read2_b64 v[46:49], v58 offset0:224 offset1:240
	v_mov_b32_e32 v61, v53
	v_pk_mul_f32 v[60:61], v[20:21], v[60:61] op_sel:[1,0] op_sel_hi:[0,1]
	v_pk_fma_f32 v[52:53], v[20:21], v[52:53], v[60:61] op_sel_hi:[1,0,1]
	s_waitcnt lgkmcnt(0)
	v_xor_b32_e32 v61, 0x80000000, v46
	v_mov_b32_e32 v60, v47
	v_pk_mul_f32 v[60:61], v[60:61], v[52:53] op_sel:[0,1]
	s_nop 0
	v_pk_fma_f32 v[46:47], v[46:47], v[52:53], v[60:61] op_sel_hi:[1,0,1]
	v_xor_b32_e32 v60, 0x80000000, v53
	v_mov_b32_e32 v61, v53
	v_pk_mul_f32 v[60:61], v[20:21], v[60:61] op_sel:[1,0] op_sel_hi:[0,1]
	v_pk_fma_f32 v[52:53], v[20:21], v[52:53], v[60:61] op_sel_hi:[1,0,1]
	v_xor_b32_e32 v61, 0x80000000, v48
	v_mov_b32_e32 v60, v49
	v_pk_mul_f32 v[60:61], v[60:61], v[52:53] op_sel:[0,1]
	s_nop 0
	v_pk_fma_f32 v[48:49], v[48:49], v[52:53], v[60:61] op_sel_hi:[1,0,1]
	v_xor_b32_e32 v60, 0x80000000, v53
	v_mov_b32_e32 v61, v53
	v_pk_mul_f32 v[60:61], v[20:21], v[60:61] op_sel:[1,0] op_sel_hi:[0,1]
	v_pk_fma_f32 v[64:65], v[20:21], v[52:53], v[60:61] op_sel_hi:[1,0,1]
	v_xad_u32 v52, v50, 8, v10
	v_lshl_add_u32 v52, v52, 3, 0
	v_add_u32_e32 v59, 0x800, v52
	ds_read2_b64 v[60:63], v59 offset1:16
	v_xor_b32_e32 v52, 0x80000000, v65
	v_mov_b32_e32 v53, v65
	v_pk_mul_f32 v[66:67], v[20:21], v[52:53] op_sel:[1,0] op_sel_hi:[0,1]
	v_pk_fma_f32 v[66:67], v[20:21], v[64:65], v[66:67] op_sel_hi:[1,0,1]
	s_waitcnt lgkmcnt(0)
	v_xor_b32_e32 v53, 0x80000000, v60
	v_mov_b32_e32 v52, v61
	v_pk_mul_f32 v[52:53], v[52:53], v[64:65] op_sel:[0,1]
	v_xor_b32_e32 v68, 0x80000000, v67
	v_pk_fma_f32 v[52:53], v[60:61], v[64:65], v[52:53] op_sel_hi:[1,0,1]
	v_xor_b32_e32 v61, 0x80000000, v62
	v_mov_b32_e32 v60, v63
	v_pk_mul_f32 v[60:61], v[60:61], v[66:67] op_sel:[0,1]
	v_mov_b32_e32 v69, v67
	v_pk_fma_f32 v[70:71], v[62:63], v[66:67], v[60:61] op_sel_hi:[1,0,1]
	v_xad_u32 v60, v50, 9, v10
	v_lshl_add_u32 v60, v60, 3, 0
	v_add_u32_e32 v60, 0x800, v60
	ds_read2_b64 v[62:65], v60 offset0:32 offset1:48
	v_pk_mul_f32 v[68:69], v[20:21], v[68:69] op_sel:[1,0] op_sel_hi:[0,1]
	v_pk_fma_f32 v[66:67], v[20:21], v[66:67], v[68:69] op_sel_hi:[1,0,1]
	s_waitcnt lgkmcnt(0)
	v_xor_b32_e32 v69, 0x80000000, v62
	v_mov_b32_e32 v68, v63
	v_pk_mul_f32 v[68:69], v[68:69], v[66:67] op_sel:[0,1]
	s_nop 0
	v_pk_fma_f32 v[72:73], v[62:63], v[66:67], v[68:69] op_sel_hi:[1,0,1]
	v_xor_b32_e32 v62, 0x80000000, v67
	v_mov_b32_e32 v63, v67
	v_pk_mul_f32 v[62:63], v[20:21], v[62:63] op_sel:[1,0] op_sel_hi:[0,1]
	v_pk_fma_f32 v[62:63], v[20:21], v[66:67], v[62:63] op_sel_hi:[1,0,1]
	v_xor_b32_e32 v67, 0x80000000, v64
	v_mov_b32_e32 v66, v65
	v_pk_mul_f32 v[66:67], v[66:67], v[62:63] op_sel:[0,1]
	s_nop 0
	v_pk_fma_f32 v[74:75], v[64:65], v[62:63], v[66:67] op_sel_hi:[1,0,1]
	v_xor_b32_e32 v64, 0x80000000, v63
	v_mov_b32_e32 v65, v63
	v_pk_mul_f32 v[64:65], v[20:21], v[64:65] op_sel:[1,0] op_sel_hi:[0,1]
	v_pk_fma_f32 v[66:67], v[20:21], v[62:63], v[64:65] op_sel_hi:[1,0,1]
	v_xad_u32 v61, v50, 10, v10
	v_lshl_add_u32 v61, v61, 3, 0
	v_add_u32_e32 v61, 0x800, v61
	ds_read2_b64 v[62:65], v61 offset0:64 offset1:80
	v_xor_b32_e32 v68, 0x80000000, v67
	v_mov_b32_e32 v69, v67
	v_pk_mul_f32 v[68:69], v[20:21], v[68:69] op_sel:[1,0] op_sel_hi:[0,1]
	v_pk_fma_f32 v[68:69], v[20:21], v[66:67], v[68:69] op_sel_hi:[1,0,1]
	s_waitcnt lgkmcnt(0)
	v_xor_b32_e32 v77, 0x80000000, v62
	v_mov_b32_e32 v76, v63
	v_pk_mul_f32 v[76:77], v[76:77], v[66:67] op_sel:[0,1]
	v_xor_b32_e32 v80, 0x80000000, v69
	v_pk_fma_f32 v[76:77], v[62:63], v[66:67], v[76:77] op_sel_hi:[1,0,1]
	v_xor_b32_e32 v63, 0x80000000, v64
	v_mov_b32_e32 v62, v65
	v_pk_mul_f32 v[62:63], v[62:63], v[68:69] op_sel:[0,1]
	v_mov_b32_e32 v81, v69
	v_pk_fma_f32 v[78:79], v[64:65], v[68:69], v[62:63] op_sel_hi:[1,0,1]
	v_xad_u32 v62, v50, 11, v10
	v_lshl_add_u32 v62, v62, 3, 0
	v_add_u32_e32 v62, 0x800, v62
	ds_read2_b64 v[64:67], v62 offset0:96 offset1:112
	v_pk_mul_f32 v[80:81], v[20:21], v[80:81] op_sel:[1,0] op_sel_hi:[0,1]
	v_pk_fma_f32 v[68:69], v[20:21], v[68:69], v[80:81] op_sel_hi:[1,0,1]
	s_waitcnt lgkmcnt(0)
	v_xor_b32_e32 v81, 0x80000000, v64
	v_mov_b32_e32 v80, v65
	v_pk_mul_f32 v[80:81], v[80:81], v[68:69] op_sel:[0,1]
	s_nop 0
	v_pk_fma_f32 v[80:81], v[64:65], v[68:69], v[80:81] op_sel_hi:[1,0,1]
	v_xor_b32_e32 v64, 0x80000000, v69
	v_mov_b32_e32 v65, v69
	v_pk_mul_f32 v[64:65], v[20:21], v[64:65] op_sel:[1,0] op_sel_hi:[0,1]
	v_pk_fma_f32 v[64:65], v[20:21], v[68:69], v[64:65] op_sel_hi:[1,0,1]
	v_xor_b32_e32 v69, 0x80000000, v66
	v_mov_b32_e32 v68, v67
	v_pk_mul_f32 v[68:69], v[68:69], v[64:65] op_sel:[0,1]
	s_nop 0
	v_pk_fma_f32 v[82:83], v[66:67], v[64:65], v[68:69] op_sel_hi:[1,0,1]
	v_xor_b32_e32 v66, 0x80000000, v65
	v_mov_b32_e32 v67, v65
	v_pk_mul_f32 v[66:67], v[20:21], v[66:67] op_sel:[1,0] op_sel_hi:[0,1]
	v_pk_fma_f32 v[68:69], v[20:21], v[64:65], v[66:67] op_sel_hi:[1,0,1]
	v_xad_u32 v63, v50, 12, v10
	v_lshl_add_u32 v63, v63, 3, 0
	v_add_u32_e32 v63, 0x800, v63
	ds_read2_b64 v[64:67], v63 offset0:128 offset1:144
	v_xor_b32_e32 v84, 0x80000000, v69
	v_mov_b32_e32 v85, v69
	v_pk_mul_f32 v[84:85], v[20:21], v[84:85] op_sel:[1,0] op_sel_hi:[0,1]
	v_pk_fma_f32 v[84:85], v[20:21], v[68:69], v[84:85] op_sel_hi:[1,0,1]
	s_waitcnt lgkmcnt(0)
	v_xor_b32_e32 v87, 0x80000000, v64
	v_mov_b32_e32 v86, v65
	v_pk_mul_f32 v[86:87], v[86:87], v[68:69] op_sel:[0,1]
	v_xor_b32_e32 v90, 0x80000000, v85
	v_pk_fma_f32 v[86:87], v[64:65], v[68:69], v[86:87] op_sel_hi:[1,0,1]
	v_xor_b32_e32 v65, 0x80000000, v66
	v_mov_b32_e32 v64, v67
	v_pk_mul_f32 v[64:65], v[64:65], v[84:85] op_sel:[0,1]
	v_mov_b32_e32 v91, v85
	v_pk_fma_f32 v[88:89], v[66:67], v[84:85], v[64:65] op_sel_hi:[1,0,1]
	v_xad_u32 v64, v50, 13, v10
	v_lshl_add_u32 v64, v64, 3, 0
	v_add_u32_e32 v64, 0x800, v64
	ds_read2_b64 v[66:69], v64 offset0:160 offset1:176
	v_pk_mul_f32 v[90:91], v[20:21], v[90:91] op_sel:[1,0] op_sel_hi:[0,1]
	v_pk_fma_f32 v[84:85], v[20:21], v[84:85], v[90:91] op_sel_hi:[1,0,1]
	s_waitcnt lgkmcnt(0)
	v_xor_b32_e32 v91, 0x80000000, v66
	v_mov_b32_e32 v90, v67
	v_pk_mul_f32 v[90:91], v[90:91], v[84:85] op_sel:[0,1]
	s_nop 0
	v_pk_fma_f32 v[90:91], v[66:67], v[84:85], v[90:91] op_sel_hi:[1,0,1]
	v_xor_b32_e32 v66, 0x80000000, v85
	v_mov_b32_e32 v67, v85
	v_pk_mul_f32 v[66:67], v[20:21], v[66:67] op_sel:[1,0] op_sel_hi:[0,1]
	v_pk_fma_f32 v[66:67], v[20:21], v[84:85], v[66:67] op_sel_hi:[1,0,1]
	v_xor_b32_e32 v85, 0x80000000, v68
	v_mov_b32_e32 v84, v69
	v_pk_mul_f32 v[84:85], v[84:85], v[66:67] op_sel:[0,1]
	s_nop 0
	v_pk_fma_f32 v[84:85], v[68:69], v[66:67], v[84:85] op_sel_hi:[1,0,1]
	v_xor_b32_e32 v68, 0x80000000, v67
	v_mov_b32_e32 v69, v67
	v_pk_mul_f32 v[68:69], v[20:21], v[68:69] op_sel:[1,0] op_sel_hi:[0,1]
	v_pk_fma_f32 v[92:93], v[20:21], v[66:67], v[68:69] op_sel_hi:[1,0,1]
	v_xad_u32 v65, v50, 14, v10
	v_lshl_add_u32 v65, v65, 3, 0
	v_add_u32_e32 v65, 0x800, v65
	ds_read2_b64 v[66:69], v65 offset0:192 offset1:208
	v_xor_b32_e32 v94, 0x80000000, v93
	v_mov_b32_e32 v95, v93
	v_pk_mul_f32 v[94:95], v[20:21], v[94:95] op_sel:[1,0] op_sel_hi:[0,1]
	v_xad_u32 v10, v50, 15, v10
	s_waitcnt lgkmcnt(0)
	v_xor_b32_e32 v97, 0x80000000, v66
	v_mov_b32_e32 v96, v67
	v_pk_mul_f32 v[96:97], v[96:97], v[92:93] op_sel:[0,1]
	v_lshl_add_u32 v10, v10, 3, 0
	v_pk_fma_f32 v[96:97], v[66:67], v[92:93], v[96:97] op_sel_hi:[1,0,1]
	v_pk_fma_f32 v[92:93], v[20:21], v[92:93], v[94:95] op_sel_hi:[1,0,1]
	v_xor_b32_e32 v67, 0x80000000, v68
	v_mov_b32_e32 v66, v69
	v_pk_mul_f32 v[66:67], v[66:67], v[92:93] op_sel:[0,1]
	v_add_u32_e32 v101, 0x800, v10
	v_pk_fma_f32 v[94:95], v[68:69], v[92:93], v[66:67] op_sel_hi:[1,0,1]
	ds_read2_b64 v[66:69], v101 offset0:224 offset1:240
	v_xor_b32_e32 v98, 0x80000000, v93
	v_mov_b32_e32 v99, v93
	v_pk_mul_f32 v[98:99], v[20:21], v[98:99] op_sel:[1,0] op_sel_hi:[0,1]
	v_pk_fma_f32 v[92:93], v[20:21], v[92:93], v[98:99] op_sel_hi:[1,0,1]
	s_waitcnt lgkmcnt(0)
	v_xor_b32_e32 v99, 0x80000000, v66
	v_mov_b32_e32 v98, v67
	v_pk_mul_f32 v[98:99], v[98:99], v[92:93] op_sel:[0,1]
	s_nop 0
	v_pk_fma_f32 v[66:67], v[66:67], v[92:93], v[98:99] op_sel_hi:[1,0,1]
	v_xor_b32_e32 v98, 0x80000000, v93
	v_mov_b32_e32 v99, v93
	v_pk_mul_f32 v[98:99], v[20:21], v[98:99] op_sel:[1,0] op_sel_hi:[0,1]
	v_pk_fma_f32 v[20:21], v[20:21], v[92:93], v[98:99] op_sel_hi:[1,0,1]
	v_xor_b32_e32 v93, 0x80000000, v68
	v_mov_b32_e32 v92, v69
	v_pk_mul_f32 v[92:93], v[92:93], v[20:21] op_sel:[0,1]
	s_nop 0
	v_pk_fma_f32 v[68:69], v[68:69], v[20:21], v[92:93] op_sel_hi:[1,0,1]
	v_mov_b32_e32 v10, v164
	v_pk_add_f32 v[104:105], v[16:17], v[52:53]
	v_pk_add_f32 v[16:17], v[16:17], v[52:53] neg_lo:[0,1] neg_hi:[0,1]
	v_pk_add_f32 v[52:53], v[18:19], v[70:71]
	v_pk_add_f32 v[18:19], v[18:19], v[70:71] neg_lo:[0,1] neg_hi:[0,1]
	v_mov_b32_e32 v92, v165
	v_mov_b32_e32 v20, v166
	v_mov_b32_e32 v98, v167
	v_mov_b32_e32 v10, v168
	v_mov_b32_e32 v100, v169
	v_mov_b32_e32 v50, v170
	v_mov_b32_e32 v102, v171
	v_xor_b32_e32 v70, 0x80000000, v19
	v_mov_b32_e32 v71, v18
	v_mov_b32_e32 v21, v172
	v_pk_mul_f32 v[70:71], v[102:103], v[70:71] op_sel_hi:[0,1]
	v_pk_fma_f32 v[18:19], v[92:93], v[18:19], v[70:71] op_sel_hi:[0,1,1]
	v_pk_add_f32 v[70:71], v[22:23], v[72:73]
	v_pk_add_f32 v[22:23], v[22:23], v[72:73] neg_lo:[0,1] neg_hi:[0,1]
	s_nop 0
	v_xor_b32_e32 v72, 0x80000000, v23
	v_mov_b32_e32 v73, v22
	v_pk_mul_f32 v[72:73], v[50:51], v[72:73] op_sel_hi:[0,1]
	v_pk_fma_f32 v[22:23], v[20:21], v[22:23], v[72:73] op_sel_hi:[0,1,1]
	v_pk_add_f32 v[72:73], v[24:25], v[74:75]
	v_pk_add_f32 v[24:25], v[24:25], v[74:75] neg_lo:[0,1] neg_hi:[0,1]
	s_nop 0
	v_xor_b32_e32 v74, 0x80000000, v25
	v_mov_b32_e32 v75, v24
	v_pk_mul_f32 v[74:75], v[100:101], v[74:75] op_sel_hi:[0,1]
	v_pk_fma_f32 v[24:25], v[98:99], v[24:25], v[74:75] op_sel_hi:[0,1,1]
	v_pk_add_f32 v[74:75], v[28:29], v[76:77]
	v_pk_add_f32 v[28:29], v[28:29], v[76:77] neg_lo:[0,1] neg_hi:[0,1]
	s_nop 0
	v_xor_b32_e32 v76, 0x80000000, v29
	v_mov_b32_e32 v77, v28
	v_pk_mul_f32 v[76:77], v[10:11], v[76:77] op_sel_hi:[0,1]
	v_pk_fma_f32 v[28:29], v[10:11], v[28:29], v[76:77] op_sel_hi:[0,1,1]
	v_pk_add_f32 v[76:77], v[26:27], v[78:79]
	v_pk_add_f32 v[26:27], v[26:27], v[78:79] neg_lo:[0,1] neg_hi:[0,1]
	s_nop 0
	v_xor_b32_e32 v78, 0x80000000, v27
	v_mov_b32_e32 v79, v26
	v_pk_mul_f32 v[78:79], v[98:99], v[78:79] op_sel_hi:[0,1]
	v_pk_fma_f32 v[26:27], v[100:101], v[26:27], v[78:79] op_sel_hi:[0,1,1]
	v_pk_add_f32 v[78:79], v[30:31], v[80:81]
	v_pk_add_f32 v[30:31], v[30:31], v[80:81] neg_lo:[0,1] neg_hi:[0,1]
	s_nop 0
	v_xor_b32_e32 v80, 0x80000000, v31
	v_mov_b32_e32 v81, v30
	v_pk_mul_f32 v[80:81], v[20:21], v[80:81] op_sel_hi:[0,1]
	v_pk_fma_f32 v[30:31], v[50:51], v[30:31], v[80:81] op_sel_hi:[0,1,1]
	v_pk_add_f32 v[80:81], v[32:33], v[82:83]
	v_pk_add_f32 v[32:33], v[32:33], v[82:83] neg_lo:[0,1] neg_hi:[0,1]
	s_nop 0
	v_xor_b32_e32 v82, 0x80000000, v33
	v_mov_b32_e32 v83, v32
	v_pk_mul_f32 v[82:83], v[92:93], v[82:83] op_sel_hi:[0,1]
	v_pk_fma_f32 v[32:33], v[102:103], v[32:33], v[82:83] op_sel_hi:[0,1,1]
	v_pk_add_f32 v[82:83], v[34:35], v[86:87]
	v_pk_add_f32 v[34:35], v[34:35], v[86:87] neg_lo:[0,1] neg_hi:[0,1]
	s_nop 0
	v_xor_b32_e32 v86, 0x80000000, v35
	v_mov_b32_e32 v87, v34
	v_pk_add_f32 v[34:35], v[36:37], v[88:89]
	v_pk_add_f32 v[36:37], v[36:37], v[88:89] neg_lo:[0,1] neg_hi:[0,1]
	s_nop 0
	v_xor_b32_e32 v88, 0x80000000, v37
	v_mov_b32_e32 v89, v36
	v_pk_mul_f32 v[88:89], v[92:93], v[88:89] op_sel_hi:[0,1]
	v_pk_fma_f32 v[36:37], v[102:103], v[36:37], v[88:89] op_sel_hi:[0,1,1] neg_lo:[1,0,0] neg_hi:[1,0,0]
	v_pk_add_f32 v[88:89], v[38:39], v[90:91]
	v_pk_add_f32 v[38:39], v[38:39], v[90:91] neg_lo:[0,1] neg_hi:[0,1]
	s_nop 0
	v_xor_b32_e32 v90, 0x80000000, v39
	v_mov_b32_e32 v91, v38
	v_pk_mul_f32 v[90:91], v[20:21], v[90:91] op_sel_hi:[0,1]
	v_pk_fma_f32 v[38:39], v[50:51], v[38:39], v[90:91] op_sel_hi:[0,1,1] neg_lo:[1,0,0] neg_hi:[1,0,0]
	v_pk_add_f32 v[90:91], v[40:41], v[84:85]
	v_pk_add_f32 v[40:41], v[40:41], v[84:85] neg_lo:[0,1] neg_hi:[0,1]
	s_nop 0
	v_xor_b32_e32 v84, 0x80000000, v41
	v_mov_b32_e32 v85, v40
	v_pk_mul_f32 v[84:85], v[98:99], v[84:85] op_sel_hi:[0,1]
	v_pk_fma_f32 v[40:41], v[100:101], v[40:41], v[84:85] op_sel_hi:[0,1,1] neg_lo:[1,0,0] neg_hi:[1,0,0]
	v_pk_add_f32 v[84:85], v[44:45], v[96:97]
	v_pk_add_f32 v[44:45], v[44:45], v[96:97] neg_lo:[0,1] neg_hi:[0,1]
	s_nop 0
	v_xor_b32_e32 v96, 0x80000000, v45
	v_mov_b32_e32 v97, v44
	v_pk_mul_f32 v[96:97], v[10:11], v[96:97] op_sel_hi:[0,1]
	v_pk_fma_f32 v[44:45], v[10:11], v[44:45], v[96:97] op_sel_hi:[0,1,1] neg_lo:[1,0,0] neg_hi:[1,0,0]
	v_pk_add_f32 v[96:97], v[42:43], v[94:95]
	v_pk_add_f32 v[42:43], v[42:43], v[94:95] neg_lo:[0,1] neg_hi:[0,1]
	s_nop 0
	v_xor_b32_e32 v94, 0x80000000, v43
	v_mov_b32_e32 v95, v42
	v_pk_mul_f32 v[94:95], v[100:101], v[94:95] op_sel_hi:[0,1]
	v_pk_fma_f32 v[42:43], v[98:99], v[42:43], v[94:95] op_sel_hi:[0,1,1] neg_lo:[1,0,0] neg_hi:[1,0,0]
	v_pk_add_f32 v[94:95], v[46:47], v[66:67]
	v_pk_add_f32 v[46:47], v[46:47], v[66:67] neg_lo:[0,1] neg_hi:[0,1]
	s_nop 0
	v_xor_b32_e32 v66, 0x80000000, v47
	v_mov_b32_e32 v67, v46
	v_pk_mul_f32 v[66:67], v[50:51], v[66:67] op_sel_hi:[0,1]
	v_pk_fma_f32 v[46:47], v[20:21], v[46:47], v[66:67] op_sel_hi:[0,1,1] neg_lo:[1,0,0] neg_hi:[1,0,0]
	v_pk_add_f32 v[66:67], v[48:49], v[68:69]
	v_pk_add_f32 v[48:49], v[48:49], v[68:69] neg_lo:[0,1] neg_hi:[0,1]
	s_nop 0
	v_xor_b32_e32 v68, 0x80000000, v49
	v_mov_b32_e32 v69, v48
	v_pk_mul_f32 v[68:69], v[102:103], v[68:69] op_sel_hi:[0,1]
	v_pk_fma_f32 v[48:49], v[92:93], v[48:49], v[68:69] op_sel_hi:[0,1,1] neg_lo:[1,0,0] neg_hi:[1,0,0]
	v_pk_add_f32 v[92:93], v[52:53], v[34:35]
	v_pk_add_f32 v[34:35], v[52:53], v[34:35] neg_lo:[0,1] neg_hi:[0,1]
	v_pk_add_f32 v[68:69], v[104:105], v[82:83]
	v_xor_b32_e32 v52, 0x80000000, v35
	v_mov_b32_e32 v53, v34
	v_pk_mul_f32 v[52:53], v[50:51], v[52:53] op_sel_hi:[0,1]
	v_pk_fma_f32 v[34:35], v[20:21], v[34:35], v[52:53] op_sel_hi:[0,1,1]
	v_pk_add_f32 v[52:53], v[70:71], v[88:89]
	v_pk_add_f32 v[70:71], v[70:71], v[88:89] neg_lo:[0,1] neg_hi:[0,1]
	v_pk_add_f32 v[82:83], v[104:105], v[82:83] neg_lo:[0,1] neg_hi:[0,1]
	v_xor_b32_e32 v88, 0x80000000, v71
	v_mov_b32_e32 v89, v70
	v_pk_mul_f32 v[88:89], v[10:11], v[88:89] op_sel_hi:[0,1]
	v_pk_fma_f32 v[70:71], v[10:11], v[70:71], v[88:89] op_sel_hi:[0,1,1]
	v_pk_add_f32 v[88:89], v[72:73], v[90:91]
	v_pk_add_f32 v[72:73], v[72:73], v[90:91] neg_lo:[0,1] neg_hi:[0,1]
	s_nop 0
	v_xor_b32_e32 v90, 0x80000000, v73
	v_mov_b32_e32 v91, v72
	v_pk_mul_f32 v[90:91], v[20:21], v[90:91] op_sel_hi:[0,1]
	v_pk_fma_f32 v[72:73], v[50:51], v[72:73], v[90:91] op_sel_hi:[0,1,1]
	v_pk_add_f32 v[90:91], v[74:75], v[84:85]
	v_pk_add_f32 v[74:75], v[74:75], v[84:85] neg_lo:[0,1] neg_hi:[0,1]
	s_nop 0
	v_xor_b32_e32 v84, 0x80000000, v75
	v_mov_b32_e32 v85, v74
	v_pk_add_f32 v[74:75], v[76:77], v[96:97]
	v_pk_add_f32 v[76:77], v[76:77], v[96:97] neg_lo:[0,1] neg_hi:[0,1]
	s_nop 0
	v_xor_b32_e32 v96, 0x80000000, v77
	v_mov_b32_e32 v97, v76
	v_pk_mul_f32 v[96:97], v[20:21], v[96:97] op_sel_hi:[0,1]
	v_pk_fma_f32 v[76:77], v[50:51], v[76:77], v[96:97] op_sel_hi:[0,1,1] neg_lo:[1,0,0] neg_hi:[1,0,0]
	v_pk_add_f32 v[96:97], v[78:79], v[94:95]
	v_pk_add_f32 v[78:79], v[78:79], v[94:95] neg_lo:[0,1] neg_hi:[0,1]
	s_nop 0
	v_xor_b32_e32 v94, 0x80000000, v79
	v_mov_b32_e32 v95, v78
	v_pk_mul_f32 v[94:95], v[10:11], v[94:95] op_sel_hi:[0,1]
	v_pk_fma_f32 v[78:79], v[10:11], v[78:79], v[94:95] op_sel_hi:[0,1,1] neg_lo:[1,0,0] neg_hi:[1,0,0]
	v_pk_add_f32 v[94:95], v[80:81], v[66:67]
	v_pk_add_f32 v[66:67], v[80:81], v[66:67] neg_lo:[0,1] neg_hi:[0,1]
	s_nop 0
	v_xor_b32_e32 v80, 0x80000000, v67
	v_mov_b32_e32 v81, v66
	v_pk_mul_f32 v[80:81], v[50:51], v[80:81] op_sel_hi:[0,1]
	v_pk_fma_f32 v[66:67], v[20:21], v[66:67], v[80:81] op_sel_hi:[0,1,1] neg_lo:[1,0,0] neg_hi:[1,0,0]
	v_pk_add_f32 v[80:81], v[68:69], v[90:91]
	v_pk_add_f32 v[68:69], v[68:69], v[90:91] neg_lo:[0,1] neg_hi:[0,1]
	v_pk_add_f32 v[90:91], v[92:93], v[74:75]
	v_pk_add_f32 v[74:75], v[92:93], v[74:75] neg_lo:[0,1] neg_hi:[0,1]
	s_nop 0
	v_xor_b32_e32 v92, 0x80000000, v75
	v_mov_b32_e32 v93, v74
	v_pk_mul_f32 v[92:93], v[10:11], v[92:93] op_sel_hi:[0,1]
	v_pk_fma_f32 v[74:75], v[10:11], v[74:75], v[92:93] op_sel_hi:[0,1,1]
	v_pk_add_f32 v[92:93], v[52:53], v[96:97]
	v_pk_add_f32 v[52:53], v[52:53], v[96:97] neg_lo:[0,1] neg_hi:[0,1]
	s_nop 0
	v_xor_b32_e32 v96, 0x80000000, v53
	v_mov_b32_e32 v97, v52
	v_pk_add_f32 v[52:53], v[88:89], v[94:95]
	v_pk_add_f32 v[88:89], v[88:89], v[94:95] neg_lo:[0,1] neg_hi:[0,1]
	s_nop 0
	v_xor_b32_e32 v94, 0x80000000, v89
	v_mov_b32_e32 v95, v88
	v_pk_mul_f32 v[94:95], v[10:11], v[94:95] op_sel_hi:[0,1]
	v_pk_fma_f32 v[88:89], v[10:11], v[88:89], v[94:95] op_sel_hi:[0,1,1] neg_lo:[1,0,0] neg_hi:[1,0,0]
	v_pk_add_f32 v[94:95], v[80:81], v[92:93]
	v_pk_add_f32 v[80:81], v[80:81], v[92:93] neg_lo:[0,1] neg_hi:[0,1]
	v_pk_add_f32 v[92:93], v[90:91], v[52:53]
	v_pk_add_f32 v[52:53], v[90:91], v[52:53] neg_lo:[0,1] neg_hi:[0,1]
	s_nop 0
	v_xor_b32_e32 v90, 0x80000000, v53
	v_mov_b32_e32 v91, v52
	v_pk_add_f32 v[52:53], v[94:95], v[92:93]
	v_pk_add_f32 v[92:93], v[94:95], v[92:93] neg_lo:[0,1] neg_hi:[0,1]
	v_pk_add_f32 v[94:95], v[80:81], v[90:91]
	v_pk_add_f32 v[80:81], v[80:81], v[90:91] neg_lo:[0,1] neg_hi:[0,1]
	v_pk_add_f32 v[90:91], v[68:69], v[96:97]
	v_pk_add_f32 v[68:69], v[68:69], v[96:97] neg_lo:[0,1] neg_hi:[0,1]
	v_pk_add_f32 v[96:97], v[74:75], v[88:89]
	v_pk_add_f32 v[74:75], v[74:75], v[88:89] neg_lo:[0,1] neg_hi:[0,1]
	s_nop 0
	v_xor_b32_e32 v88, 0x80000000, v75
	v_mov_b32_e32 v89, v74
	v_pk_add_f32 v[74:75], v[90:91], v[96:97]
	v_pk_add_f32 v[90:91], v[90:91], v[96:97] neg_lo:[0,1] neg_hi:[0,1]
	v_pk_add_f32 v[96:97], v[68:69], v[88:89]
	v_pk_add_f32 v[68:69], v[68:69], v[88:89] neg_lo:[0,1] neg_hi:[0,1]
	v_pk_add_f32 v[88:89], v[82:83], v[84:85]
	v_pk_add_f32 v[82:83], v[82:83], v[84:85] neg_lo:[0,1] neg_hi:[0,1]
	v_pk_add_f32 v[84:85], v[34:35], v[76:77]
	v_pk_add_f32 v[34:35], v[34:35], v[76:77] neg_lo:[0,1] neg_hi:[0,1]
	s_nop 0
	v_xor_b32_e32 v76, 0x80000000, v35
	v_mov_b32_e32 v77, v34
	v_pk_mul_f32 v[76:77], v[10:11], v[76:77] op_sel_hi:[0,1]
	v_pk_fma_f32 v[34:35], v[10:11], v[34:35], v[76:77] op_sel_hi:[0,1,1]
	v_pk_add_f32 v[76:77], v[70:71], v[78:79]
	v_pk_add_f32 v[70:71], v[70:71], v[78:79] neg_lo:[0,1] neg_hi:[0,1]
	s_nop 0
	v_xor_b32_e32 v78, 0x80000000, v71
	v_mov_b32_e32 v79, v70
	v_pk_add_f32 v[70:71], v[72:73], v[66:67]
	v_pk_add_f32 v[66:67], v[72:73], v[66:67] neg_lo:[0,1] neg_hi:[0,1]
	s_nop 0
	v_xor_b32_e32 v72, 0x80000000, v67
	v_mov_b32_e32 v73, v66
	v_pk_mul_f32 v[72:73], v[10:11], v[72:73] op_sel_hi:[0,1]
	v_pk_fma_f32 v[66:67], v[10:11], v[66:67], v[72:73] op_sel_hi:[0,1,1] neg_lo:[1,0,0] neg_hi:[1,0,0]
	v_pk_add_f32 v[72:73], v[88:89], v[76:77]
	v_pk_add_f32 v[76:77], v[88:89], v[76:77] neg_lo:[0,1] neg_hi:[0,1]
	v_pk_add_f32 v[88:89], v[84:85], v[70:71]
	v_pk_add_f32 v[70:71], v[84:85], v[70:71] neg_lo:[0,1] neg_hi:[0,1]
	s_nop 0
	v_xor_b32_e32 v84, 0x80000000, v71
	v_mov_b32_e32 v85, v70
	v_pk_add_f32 v[70:71], v[72:73], v[88:89]
	v_pk_add_f32 v[72:73], v[72:73], v[88:89] neg_lo:[0,1] neg_hi:[0,1]
	v_pk_add_f32 v[88:89], v[76:77], v[84:85]
	v_pk_add_f32 v[76:77], v[76:77], v[84:85] neg_lo:[0,1] neg_hi:[0,1]
	v_pk_add_f32 v[84:85], v[82:83], v[78:79]
	v_pk_add_f32 v[78:79], v[82:83], v[78:79] neg_lo:[0,1] neg_hi:[0,1]
	v_pk_add_f32 v[82:83], v[34:35], v[66:67]
	v_pk_add_f32 v[34:35], v[34:35], v[66:67] neg_lo:[0,1] neg_hi:[0,1]
	s_nop 0
	v_xor_b32_e32 v66, 0x80000000, v35
	v_mov_b32_e32 v67, v34
	v_pk_add_f32 v[34:35], v[84:85], v[82:83]
	v_pk_add_f32 v[82:83], v[84:85], v[82:83] neg_lo:[0,1] neg_hi:[0,1]
	v_pk_add_f32 v[84:85], v[78:79], v[66:67]
	v_pk_add_f32 v[66:67], v[78:79], v[66:67] neg_lo:[0,1] neg_hi:[0,1]
	v_pk_add_f32 v[78:79], v[16:17], v[86:87]
	v_pk_add_f32 v[16:17], v[16:17], v[86:87] neg_lo:[0,1] neg_hi:[0,1]
	v_pk_add_f32 v[86:87], v[18:19], v[36:37]
	v_pk_add_f32 v[18:19], v[18:19], v[36:37] neg_lo:[0,1] neg_hi:[0,1]
	s_nop 0
	v_xor_b32_e32 v36, 0x80000000, v19
	v_mov_b32_e32 v37, v18
	v_pk_mul_f32 v[36:37], v[50:51], v[36:37] op_sel_hi:[0,1]
	v_pk_fma_f32 v[18:19], v[20:21], v[18:19], v[36:37] op_sel_hi:[0,1,1]
	v_pk_add_f32 v[36:37], v[22:23], v[38:39]
	v_pk_add_f32 v[22:23], v[22:23], v[38:39] neg_lo:[0,1] neg_hi:[0,1]
	s_nop 0
	v_xor_b32_e32 v38, 0x80000000, v23
	v_mov_b32_e32 v39, v22
	v_pk_mul_f32 v[38:39], v[10:11], v[38:39] op_sel_hi:[0,1]
	v_pk_fma_f32 v[22:23], v[10:11], v[22:23], v[38:39] op_sel_hi:[0,1,1]
	v_pk_add_f32 v[38:39], v[24:25], v[40:41]
	v_pk_add_f32 v[24:25], v[24:25], v[40:41] neg_lo:[0,1] neg_hi:[0,1]
	s_nop 0
	v_xor_b32_e32 v40, 0x80000000, v25
	v_mov_b32_e32 v41, v24
	v_pk_mul_f32 v[40:41], v[20:21], v[40:41] op_sel_hi:[0,1]
	v_pk_fma_f32 v[24:25], v[50:51], v[24:25], v[40:41] op_sel_hi:[0,1,1]
	v_pk_add_f32 v[40:41], v[28:29], v[44:45]
	v_pk_add_f32 v[28:29], v[28:29], v[44:45] neg_lo:[0,1] neg_hi:[0,1]
	s_nop 0
	v_xor_b32_e32 v44, 0x80000000, v29
	v_mov_b32_e32 v45, v28
	v_pk_add_f32 v[28:29], v[26:27], v[42:43]
	v_pk_add_f32 v[26:27], v[26:27], v[42:43] neg_lo:[0,1] neg_hi:[0,1]
	s_nop 0
	v_xor_b32_e32 v42, 0x80000000, v27
	v_mov_b32_e32 v43, v26
	v_pk_mul_f32 v[42:43], v[20:21], v[42:43] op_sel_hi:[0,1]
	v_pk_fma_f32 v[26:27], v[50:51], v[26:27], v[42:43] op_sel_hi:[0,1,1] neg_lo:[1,0,0] neg_hi:[1,0,0]
	v_pk_add_f32 v[42:43], v[30:31], v[46:47]
	v_pk_add_f32 v[30:31], v[30:31], v[46:47] neg_lo:[0,1] neg_hi:[0,1]
	s_nop 0
	v_xor_b32_e32 v46, 0x80000000, v31
	v_mov_b32_e32 v47, v30
	v_pk_mul_f32 v[46:47], v[10:11], v[46:47] op_sel_hi:[0,1]
	v_pk_fma_f32 v[30:31], v[10:11], v[30:31], v[46:47] op_sel_hi:[0,1,1] neg_lo:[1,0,0] neg_hi:[1,0,0]
	v_pk_add_f32 v[46:47], v[32:33], v[48:49]
	v_pk_add_f32 v[32:33], v[32:33], v[48:49] neg_lo:[0,1] neg_hi:[0,1]
	s_nop 0
	v_xor_b32_e32 v48, 0x80000000, v33
	v_mov_b32_e32 v49, v32
	v_pk_mul_f32 v[48:49], v[50:51], v[48:49] op_sel_hi:[0,1]
	v_pk_fma_f32 v[20:21], v[20:21], v[32:33], v[48:49] op_sel_hi:[0,1,1] neg_lo:[1,0,0] neg_hi:[1,0,0]
	v_pk_add_f32 v[48:49], v[86:87], v[28:29]
	v_pk_add_f32 v[28:29], v[86:87], v[28:29] neg_lo:[0,1] neg_hi:[0,1]
	v_pk_add_f32 v[32:33], v[78:79], v[40:41]
	v_pk_add_f32 v[40:41], v[78:79], v[40:41] neg_lo:[0,1] neg_hi:[0,1]
	v_xor_b32_e32 v78, 0x80000000, v29
	v_mov_b32_e32 v79, v28
	v_pk_mul_f32 v[78:79], v[10:11], v[78:79] op_sel_hi:[0,1]
	v_pk_fma_f32 v[28:29], v[10:11], v[28:29], v[78:79] op_sel_hi:[0,1,1]
	v_pk_add_f32 v[78:79], v[36:37], v[42:43]
	v_pk_add_f32 v[36:37], v[36:37], v[42:43] neg_lo:[0,1] neg_hi:[0,1]
	s_nop 0
	v_xor_b32_e32 v42, 0x80000000, v37
	v_mov_b32_e32 v43, v36
	v_pk_add_f32 v[36:37], v[38:39], v[46:47]
	v_pk_add_f32 v[38:39], v[38:39], v[46:47] neg_lo:[0,1] neg_hi:[0,1]
	s_nop 0
	v_xor_b32_e32 v46, 0x80000000, v39
	v_mov_b32_e32 v47, v38
	v_pk_mul_f32 v[46:47], v[10:11], v[46:47] op_sel_hi:[0,1]
	v_pk_fma_f32 v[38:39], v[10:11], v[38:39], v[46:47] op_sel_hi:[0,1,1] neg_lo:[1,0,0] neg_hi:[1,0,0]
	v_pk_add_f32 v[46:47], v[32:33], v[78:79]
	v_pk_add_f32 v[32:33], v[32:33], v[78:79] neg_lo:[0,1] neg_hi:[0,1]
	v_pk_add_f32 v[78:79], v[48:49], v[36:37]
	v_pk_add_f32 v[36:37], v[48:49], v[36:37] neg_lo:[0,1] neg_hi:[0,1]
	s_nop 0
	v_xor_b32_e32 v48, 0x80000000, v37
	v_mov_b32_e32 v49, v36
	v_pk_add_f32 v[86:87], v[32:33], v[48:49]
	v_pk_add_f32 v[32:33], v[32:33], v[48:49] neg_lo:[0,1] neg_hi:[0,1]
	v_pk_add_f32 v[48:49], v[40:41], v[42:43]
	v_pk_add_f32 v[40:41], v[40:41], v[42:43] neg_lo:[0,1] neg_hi:[0,1]
	v_pk_add_f32 v[42:43], v[28:29], v[38:39]
	v_pk_add_f32 v[28:29], v[28:29], v[38:39] neg_lo:[0,1] neg_hi:[0,1]
	v_pk_add_f32 v[36:37], v[46:47], v[78:79] neg_lo:[0,1] neg_hi:[0,1]
	v_xor_b32_e32 v38, 0x80000000, v29
	v_mov_b32_e32 v39, v28
	v_pk_add_f32 v[28:29], v[48:49], v[42:43]
	v_pk_add_f32 v[42:43], v[48:49], v[42:43] neg_lo:[0,1] neg_hi:[0,1]
	v_pk_add_f32 v[48:49], v[40:41], v[38:39]
	v_pk_add_f32 v[38:39], v[40:41], v[38:39] neg_lo:[0,1] neg_hi:[0,1]
	v_pk_add_f32 v[40:41], v[16:17], v[44:45]
	v_pk_add_f32 v[16:17], v[16:17], v[44:45] neg_lo:[0,1] neg_hi:[0,1]
	v_pk_add_f32 v[44:45], v[18:19], v[26:27]
	v_pk_add_f32 v[18:19], v[18:19], v[26:27] neg_lo:[0,1] neg_hi:[0,1]
	s_nop 0
	v_xor_b32_e32 v26, 0x80000000, v19
	v_mov_b32_e32 v27, v18
	v_pk_mul_f32 v[26:27], v[10:11], v[26:27] op_sel_hi:[0,1]
	v_pk_fma_f32 v[18:19], v[10:11], v[18:19], v[26:27] op_sel_hi:[0,1,1]
	v_pk_add_f32 v[26:27], v[22:23], v[30:31]
	v_pk_add_f32 v[22:23], v[22:23], v[30:31] neg_lo:[0,1] neg_hi:[0,1]
	s_nop 0
	v_xor_b32_e32 v30, 0x80000000, v23
	v_mov_b32_e32 v31, v22
	v_pk_add_f32 v[22:23], v[24:25], v[20:21]
	v_pk_add_f32 v[20:21], v[24:25], v[20:21] neg_lo:[0,1] neg_hi:[0,1]
	s_nop 0
	v_xor_b32_e32 v24, 0x80000000, v21
	v_mov_b32_e32 v25, v20
	v_pk_mul_f32 v[24:25], v[10:11], v[24:25] op_sel_hi:[0,1]
	v_pk_fma_f32 v[20:21], v[10:11], v[20:21], v[24:25] op_sel_hi:[0,1,1] neg_lo:[1,0,0] neg_hi:[1,0,0]
	v_pk_add_f32 v[24:25], v[40:41], v[26:27]
	v_pk_add_f32 v[26:27], v[40:41], v[26:27] neg_lo:[0,1] neg_hi:[0,1]
	v_pk_add_f32 v[40:41], v[44:45], v[22:23]
	v_pk_add_f32 v[22:23], v[44:45], v[22:23] neg_lo:[0,1] neg_hi:[0,1]
	s_nop 0
	v_xor_b32_e32 v44, 0x80000000, v23
	v_mov_b32_e32 v45, v22
	v_pk_add_f32 v[22:23], v[24:25], v[40:41]
	v_pk_add_f32 v[24:25], v[24:25], v[40:41] neg_lo:[0,1] neg_hi:[0,1]
	v_pk_add_f32 v[40:41], v[26:27], v[44:45]
	v_pk_add_f32 v[26:27], v[26:27], v[44:45] neg_lo:[0,1] neg_hi:[0,1]
	v_pk_add_f32 v[44:45], v[16:17], v[30:31]
	v_pk_add_f32 v[16:17], v[16:17], v[30:31] neg_lo:[0,1] neg_hi:[0,1]
	v_pk_add_f32 v[30:31], v[18:19], v[20:21]
	v_pk_add_f32 v[18:19], v[18:19], v[20:21] neg_lo:[0,1] neg_hi:[0,1]
	s_nop 0
	v_xor_b32_e32 v20, 0x80000000, v19
	v_mov_b32_e32 v21, v18
	v_pk_add_f32 v[18:19], v[44:45], v[30:31]
	v_pk_add_f32 v[30:31], v[44:45], v[30:31] neg_lo:[0,1] neg_hi:[0,1]
	v_pk_add_f32 v[44:45], v[16:17], v[20:21]
	v_pk_add_f32 v[16:17], v[16:17], v[20:21] neg_lo:[0,1] neg_hi:[0,1]
	v_pk_add_f32 v[20:21], v[46:47], v[78:79]
	ds_write2_b64 v13, v[52:53], v[20:21] offset1:16
	ds_write2_b64 v15, v[70:71], v[22:23] offset0:32 offset1:48
	ds_write2_b64 v51, v[74:75], v[28:29] offset0:64 offset1:80
	ds_write2_b64 v54, v[34:35], v[18:19] offset0:96 offset1:112
	ds_write2_b64 v55, v[94:95], v[86:87] offset0:128 offset1:144
	ds_write2_b64 v56, v[88:89], v[40:41] offset0:160 offset1:176
	ds_write2_b64 v57, v[96:97], v[48:49] offset0:192 offset1:208
	ds_write2_b64 v58, v[84:85], v[44:45] offset0:224 offset1:240
	ds_write2_b64 v59, v[92:93], v[36:37] offset1:16
	ds_write2_b64 v60, v[72:73], v[24:25] offset0:32 offset1:48
	ds_write2_b64 v61, v[90:91], v[42:43] offset0:64 offset1:80
	ds_write2_b64 v62, v[82:83], v[30:31] offset0:96 offset1:112
	ds_write2_b64 v63, v[80:81], v[32:33] offset0:128 offset1:144
	ds_write2_b64 v64, v[76:77], v[26:27] offset0:160 offset1:176
	ds_write2_b64 v65, v[68:69], v[38:39] offset0:192 offset1:208
	ds_write2_b64 v101, v[66:67], v[16:17] offset0:224 offset1:240
	v_mov_b32_e32 v10, v174
	s_waitcnt lgkmcnt(0)
	s_barrier
	v_mov_b32_e32 v58, v180
	v_mov_b32_e32 v59, v181
	v_lshl_add_u32 v10, v10, 3, 0
	ds_read_b64 v[34:35], v10
	ds_read_b64 v[36:37], v10 offset:4224
	ds_read_b64 v[38:39], v10 offset:8448
	ds_read_b64 v[40:41], v10 offset:12672
	ds_read_b64 v[42:43], v10 offset:16896
	ds_read_b64 v[44:45], v10 offset:21120
	ds_read_b64 v[50:51], v10 offset:25344
	ds_read_b64 v[52:53], v10 offset:29568
	ds_read_b64 v[54:55], v10 offset:33792
	ds_read_b64 v[56:57], v10 offset:38016
	ds_read_b64 v[64:65], v10 offset:42240
	ds_read_b64 v[74:75], v10 offset:46464
	ds_read_b64 v[76:77], v10 offset:50688
	ds_read_b64 v[78:79], v10 offset:54912
	ds_read_b64 v[80:81], v10 offset:59136
	ds_read_b64 v[82:83], v10 offset:63360
	v_add_u32_e32 v13, 0x10800, v10
	v_add_u32_e32 v15, 0x11880, v10
	v_add_u32_e32 v16, 0x12900, v10
	v_add_u32_e32 v17, 0x13980, v10
	ds_read_b64 v[84:85], v13
	ds_read_b64 v[86:87], v15
	ds_read_b64 v[88:89], v16
	ds_read_b64 v[92:93], v17
	v_add_u32_e32 v13, 0x14a00, v10
	v_add_u32_e32 v15, 0x15a80, v10
	v_add_u32_e32 v16, 0x16b00, v10
	v_add_u32_e32 v17, 0x17b80, v10
	ds_read_b64 v[96:97], v13
	ds_read_b64 v[98:99], v15
	ds_read_b64 v[94:95], v16
	ds_read_b64 v[90:91], v17
	v_add_u32_e32 v13, 0x18c00, v10
	v_add_u32_e32 v15, 0x19c80, v10
	v_add_u32_e32 v16, 0x1ad00, v10
	v_add_u32_e32 v17, 0x1bd80, v10
	ds_read_b64 v[72:73], v13
	ds_read_b64 v[70:71], v15
	ds_read_b64 v[68:69], v16
	ds_read_b64 v[66:67], v17
	v_add_u32_e32 v13, 0x1ce00, v10
	v_add_u32_e32 v15, 0x1de80, v10
	v_add_u32_e32 v16, 0x1ef00, v10
	v_add_u32_e32 v10, 0x1ff80, v10
	ds_read_b64 v[62:63], v13
	ds_read_b64 v[60:61], v15
	ds_read_b64 v[100:101], v16
	ds_read_b64 v[102:103], v10
	s_mov_b32 s45, s43
	v_mov_b32_e32 v10, v164
	s_lshl_b64 s[0:1], s[44:45], 2
	v_readlane_b32 s2, v251, 40
	s_add_u32 s0, s2, s0
	v_readlane_b32 s2, v251, 46
	v_mov_b32_e32 v24, v165
	v_mov_b32_e32 v32, v166
	v_mov_b32_e32 v28, v167
	v_mov_b32_e32 v46, v168
	v_mov_b32_e32 v48, v169
	v_mov_b32_e32 v30, v170
	v_mov_b32_e32 v26, v171
	v_mov_b32_e32 v10, v172
	v_mov_b32_e32 v16, v184
	v_mov_b32_e32 v19, v185
	s_addc_u32 s1, s2, s1
	s_waitcnt lgkmcnt(0)
	s_barrier
	global_load_dword v13, v11, s[0:1]
	s_and_b64 s[0:1], s[96:97], exec
	s_movk_i32 s0, 0x800
	s_cselect_b32 s2, 0x400, s0
	v_readlane_b32 s20, v251, 36
	s_add_i32 s4, s2, s20
	s_mul_i32 s0, s4, 0x8200
	v_readlane_b32 s3, v250, 23
	s_mul_hi_i32 s1, s4, 0x8200
	s_add_u32 s0, s3, s0
	v_readlane_b32 s3, v251, 20
	s_addc_u32 s1, s3, s1
	s_lshl_b32 s2, s2, 2
	v_mov_b32_e32 v10, s2
	v_readlane_b32 s2, v251, 50
	v_readlane_b32 s3, v251, 51
	v_readlane_b32 s5, v251, 52
	v_readlane_b32 s6, v251, 18
	v_ashrrev_i32_e32 v15, 31, v14
	v_lshl_add_u64 v[22:23], v[14:15], 2, s[72:73]
	v_cmp_lt_i32_e32 vcc, 0, v14
	global_load_dword v189, v10, s[2:3]
	s_add_i32 s2, s4, 0xc00
	s_ashr_i32 s3, s2, 31
	s_lshl_b64 s[2:3], s[2:3], 2
	s_add_u32 s2, s5, s2
	s_addc_u32 s3, s6, s3
	global_load_dword v191, v11, s[2:3]
	s_add_i32 s2, s4, 0x1800
	s_ashr_i32 s3, s2, 31
	s_lshl_b64 s[2:3], s[2:3], 2
	s_add_u32 s2, s5, s2
	s_addc_u32 s3, s6, s3
	global_load_dword v192, v11, s[2:3]
	v_readlane_b32 s2, v251, 42
	v_readlane_b32 s3, v251, 43
	v_mov_b32_e32 v17, 0
	v_lshl_add_u64 v[20:21], v[14:15], 1, s[0:1]
	v_mov_b32_e32 v18, 0
	v_readlane_b32 s21, v251, 37
	s_nop 0
	global_load_dword v193, v10, s[2:3]
	s_nop 0
	v_lshlrev_b32_e32 v234, 1, v14
	v_lshlrev_b32_e32 v235, 2, v14
	v_add_u32_e32 v235, 0x1000, v235
	global_load_dword v190, v235, s[72:73] offset:-4096
	global_load_ushort v195, v234, s[0:1] offset:-2
	global_load_ushort v196, v234, s[0:1]
	global_load_ushort v197, v234, s[0:1] offset:2
	global_load_dword v198, v235, s[66:67] offset:-4096
	global_load_dword v199, v235, s[72:73] offset:-2048
	global_load_ushort v200, v234, s[0:1] offset:1022
	global_load_ushort v201, v234, s[0:1] offset:1024
	global_load_ushort v202, v234, s[0:1] offset:1026
	global_load_dword v203, v235, s[66:67] offset:-2048
	global_load_dword v204, v235, s[72:73]
	global_load_ushort v205, v234, s[0:1] offset:2046
	global_load_ushort v206, v234, s[0:1] offset:2048
	global_load_ushort v207, v234, s[0:1] offset:2050
	global_load_dword v208, v235, s[66:67]
	global_load_dword v209, v235, s[72:73] offset:2048
	global_load_ushort v210, v234, s[0:1] offset:3070
	global_load_ushort v211, v234, s[0:1] offset:3072
	global_load_ushort v212, v234, s[0:1] offset:3074
	global_load_dword v213, v235, s[66:67] offset:2048
	v_lshlrev_b32_e32 v234, 1, v14
	v_add_u32_e32 v234, 0x1000, v234
	v_lshlrev_b32_e32 v235, 2, v14
	v_add_u32_e32 v235, 0x3000, v235
	global_load_dword v214, v235, s[72:73] offset:-4096
	global_load_ushort v215, v234, s[0:1] offset:-2
	global_load_ushort v216, v234, s[0:1]
	global_load_ushort v217, v234, s[0:1] offset:2
	global_load_dword v218, v235, s[66:67] offset:-4096
	global_load_dword v219, v235, s[72:73] offset:-2048
	global_load_ushort v220, v234, s[0:1] offset:1022
	global_load_ushort v221, v234, s[0:1] offset:1024
	global_load_ushort v222, v234, s[0:1] offset:1026
	global_load_dword v223, v235, s[66:67] offset:-2048
	global_load_dword v224, v235, s[72:73]
	global_load_ushort v225, v234, s[0:1] offset:2046
	global_load_ushort v226, v234, s[0:1] offset:2048
	global_load_ushort v227, v234, s[0:1] offset:2050
	global_load_dword v228, v235, s[66:67]
	global_load_dword v229, v235, s[72:73] offset:2048
	global_load_ushort v230, v234, s[0:1] offset:3070
	global_load_ushort v231, v234, s[0:1] offset:3072
	global_load_ushort v232, v234, s[0:1] offset:3074
	global_load_dword v233, v235, s[66:67] offset:2048
	s_waitcnt vmcnt(20)
	v_mov_b32_e32 v10, v190
	s_and_saveexec_b64 s[2:3], vcc
	s_movk_i32 s10, 0x3fff
	s_cbranch_execz .LBB0_2732
	v_mov_b32_e32 v18, v195
	s_nop 0
	v_lshlrev_b32_e32 v18, 16, v18

.LBB0_3231:
	ds_read_b128 v[142:145], v158
	ds_read_b128 v[162:165], v158 offset:1024
	ds_read_b128 v[166:169], v158 offset:2048
	ds_read_b128 v[170:173], v158 offset:3072
	s_add_u32 s26, s24, 0xfffc0080
	s_addc_u32 s27, s25, -1
	s_cmp_eq_u32 s55, 12
	s_cselect_b32 s29, s17, s27
	s_cselect_b32 s28, s51, s26
	s_cselect_b32 s27, s15, s54
	s_cselect_b32 s26, s52, s53
	v_lshl_add_u64 v[146:147], s[24:25], 0, v[134:135]
	s_add_i32 m0, s23, 0xc000
	ds_read_b128 v[174:177], v159
	ds_read_b128 v[178:181], v159 offset:1024
	ds_read_b128 v[182:185], v159 offset:2048
	ds_read_b128 v[186:189], v159 offset:3072
	ds_read_b128 v[190:193], v159 offset:4096
	ds_read_b128 v[194:197], v159 offset:5120
	ds_read_b128 v[198:201], v159 offset:6144
	ds_read_b128 v[202:205], v159 offset:7168
	global_load_lds_dwordx4 v[146:147], off
	v_lshl_add_u64 v[146:147], s[24:25], 0, v[136:137]
	s_add_i32 m0, s23, 0xe000
	s_nop 0
	global_load_lds_dwordx4 v[146:147], off
	s_waitcnt lgkmcnt(8)
	s_barrier
	s_waitcnt lgkmcnt(0)
	s_setprio 1
	s_waitcnt lgkmcnt(0)
	v_mfma_f32_16x16x32_bf16 v[126:129], v[142:145], v[174:177], v[126:129]
	v_mfma_f32_16x16x32_bf16 v[122:125], v[166:169], v[174:177], v[122:125]
	v_mfma_f32_16x16x32_bf16 v[114:117], v[142:145], v[182:185], v[114:117]
	v_mfma_f32_16x16x32_bf16 v[106:109], v[166:169], v[182:185], v[106:109]
	v_mfma_f32_16x16x32_bf16 v[98:101], v[142:145], v[190:193], v[98:101]
	v_mfma_f32_16x16x32_bf16 v[90:93], v[166:169], v[190:193], v[90:93]
	v_mfma_f32_16x16x32_bf16 v[82:85], v[142:145], v[198:201], v[82:85]
	v_mfma_f32_16x16x32_bf16 v[74:77], v[166:169], v[198:201], v[74:77]
	v_mfma_f32_16x16x32_bf16 v[126:129], v[162:165], v[178:181], v[126:129]
	v_mfma_f32_16x16x32_bf16 v[122:125], v[170:173], v[178:181], v[122:125]
	v_mfma_f32_16x16x32_bf16 v[114:117], v[162:165], v[186:189], v[114:117]
	v_mfma_f32_16x16x32_bf16 v[106:109], v[170:173], v[186:189], v[106:109]
	v_mfma_f32_16x16x32_bf16 v[98:101], v[162:165], v[194:197], v[98:101]
	v_mfma_f32_16x16x32_bf16 v[90:93], v[170:173], v[194:197], v[90:93]
	v_mfma_f32_16x16x32_bf16 v[82:85], v[162:165], v[202:205], v[82:85]
	v_mfma_f32_16x16x32_bf16 v[74:77], v[170:173], v[202:205], v[74:77]
	s_setprio 0
	s_barrier
	s_add_i32 s56, s47, s38
	v_lshl_add_u64 v[146:147], s[26:27], 0, v[130:131]
	s_mov_b32 m0, s56
	ds_read_b128 v[206:209], v160
	ds_read_b128 v[210:213], v160 offset:1024
	ds_read_b128 v[214:217], v160 offset:2048
	ds_read_b128 v[218:221], v160 offset:3072
	global_load_lds_dwordx4 v[146:147], off
	v_lshl_add_u64 v[222:223], s[26:27], 0, v[132:133]
	s_add_i32 m0, s56, 0x2000
	s_nop 0
	global_load_lds_dwordx4 v[222:223], off
	s_barrier
	s_waitcnt lgkmcnt(0)
	s_setprio 1
	s_waitcnt lgkmcnt(0)
	v_mfma_f32_16x16x32_bf16 v[118:121], v[206:209], v[174:177], v[118:121]
	v_mfma_f32_16x16x32_bf16 v[110:113], v[214:217], v[174:177], v[110:113]
	v_mfma_f32_16x16x32_bf16 v[102:105], v[206:209], v[182:185], v[102:105]
	v_mfma_f32_16x16x32_bf16 v[94:97], v[214:217], v[182:185], v[94:97]
	v_mfma_f32_16x16x32_bf16 v[86:89], v[206:209], v[190:193], v[86:89]
	v_mfma_f32_16x16x32_bf16 v[78:81], v[214:217], v[190:193], v[78:81]
	v_mfma_f32_16x16x32_bf16 v[70:73], v[206:209], v[198:201], v[70:73]
	v_mfma_f32_16x16x32_bf16 v[66:69], v[214:217], v[198:201], v[66:69]
	v_mfma_f32_16x16x32_bf16 v[118:121], v[210:213], v[178:181], v[118:121]
	v_mfma_f32_16x16x32_bf16 v[110:113], v[218:221], v[178:181], v[110:113]
	v_mfma_f32_16x16x32_bf16 v[102:105], v[210:213], v[186:189], v[102:105]
	v_mfma_f32_16x16x32_bf16 v[94:97], v[218:221], v[186:189], v[94:97]
	v_mfma_f32_16x16x32_bf16 v[86:89], v[210:213], v[194:197], v[86:89]
	v_mfma_f32_16x16x32_bf16 v[78:81], v[218:221], v[194:197], v[78:81]
	v_mfma_f32_16x16x32_bf16 v[70:73], v[210:213], v[202:205], v[70:73]
	v_mfma_f32_16x16x32_bf16 v[66:69], v[218:221], v[202:205], v[66:69]
	s_setprio 0
	s_mov_b32 m0, s23
	v_lshl_add_u64 v[224:225], s[28:29], 0, v[130:131]
	s_barrier
	ds_read_b128 v[174:177], v159 offset:16384
	ds_read_b128 v[178:181], v159 offset:17408
	ds_read_b128 v[182:185], v159 offset:18432
	ds_read_b128 v[186:189], v159 offset:19456
	ds_read_b128 v[190:193], v159 offset:20480
	ds_read_b128 v[194:197], v159 offset:21504
	ds_read_b128 v[198:201], v159 offset:22528
	ds_read_b128 v[202:205], v159 offset:23552
	global_load_lds_dwordx4 v[224:225], off
	v_lshl_add_u64 v[226:227], s[28:29], 0, v[132:133]
	s_mov_b32 m0, s40
	s_nop 0
	global_load_lds_dwordx4 v[226:227], off
	s_barrier
	s_waitcnt lgkmcnt(0)
	s_setprio 1
	s_waitcnt lgkmcnt(0)
	v_mfma_f32_16x16x32_bf16 v[62:65], v[142:145], v[174:177], v[62:65]
	v_mfma_f32_16x16x32_bf16 v[58:61], v[166:169], v[174:177], v[58:61]
	v_mfma_f32_16x16x32_bf16 v[50:53], v[142:145], v[182:185], v[50:53]
	v_mfma_f32_16x16x32_bf16 v[42:45], v[166:169], v[182:185], v[42:45]
	v_mfma_f32_16x16x32_bf16 v[34:37], v[142:145], v[190:193], v[34:37]
	v_mfma_f32_16x16x32_bf16 v[26:29], v[166:169], v[190:193], v[26:29]
	v_mfma_f32_16x16x32_bf16 v[18:21], v[142:145], v[198:201], v[18:21]
	v_mfma_f32_16x16x32_bf16 v[10:13], v[166:169], v[198:201], v[10:13]
	v_mfma_f32_16x16x32_bf16 v[62:65], v[162:165], v[178:181], v[62:65]
	v_mfma_f32_16x16x32_bf16 v[58:61], v[170:173], v[178:181], v[58:61]
	v_mfma_f32_16x16x32_bf16 v[50:53], v[162:165], v[186:189], v[50:53]
	v_mfma_f32_16x16x32_bf16 v[42:45], v[170:173], v[186:189], v[42:45]
	v_mfma_f32_16x16x32_bf16 v[34:37], v[162:165], v[194:197], v[34:37]
	v_mfma_f32_16x16x32_bf16 v[26:29], v[170:173], v[194:197], v[26:29]
	v_mfma_f32_16x16x32_bf16 v[18:21], v[162:165], v[202:205], v[18:21]
	v_mfma_f32_16x16x32_bf16 v[10:13], v[170:173], v[202:205], v[10:13]
	s_setprio 0
	s_barrier
	s_add_u32 s56, s26, 0x40000
	s_addc_u32 s57, s27, 0
	s_add_i32 s58, s48, s38
	v_lshl_add_u64 v[142:143], s[56:57], 0, v[130:131]
	s_mov_b32 m0, s58
	s_nop 0
	global_load_lds_dwordx4 v[142:143], off
	v_lshl_add_u64 v[142:143], s[56:57], 0, v[132:133]
	s_add_i32 m0, s58, 0x2000
	s_nop 0
	global_load_lds_dwordx4 v[142:143], off
	s_waitcnt vmcnt(6)
	s_barrier
	s_setprio 1
	v_mfma_f32_16x16x32_bf16 v[54:57], v[206:209], v[174:177], v[54:57]
	v_mfma_f32_16x16x32_bf16 v[46:49], v[214:217], v[174:177], v[46:49]
	v_mfma_f32_16x16x32_bf16 v[38:41], v[206:209], v[182:185], v[38:41]
	v_mfma_f32_16x16x32_bf16 v[30:33], v[214:217], v[182:185], v[30:33]
	v_mfma_f32_16x16x32_bf16 v[22:25], v[206:209], v[190:193], v[22:25]
	v_mfma_f32_16x16x32_bf16 v[14:17], v[214:217], v[190:193], v[14:17]
	v_mfma_f32_16x16x32_bf16 v[6:9], v[206:209], v[198:201], v[6:9]
	v_mfma_f32_16x16x32_bf16 v[2:5], v[214:217], v[198:201], v[2:5]
	v_mfma_f32_16x16x32_bf16 v[54:57], v[210:213], v[178:181], v[54:57]
	v_mfma_f32_16x16x32_bf16 v[46:49], v[218:221], v[178:181], v[46:49]
	v_mfma_f32_16x16x32_bf16 v[38:41], v[210:213], v[186:189], v[38:41]
	v_mfma_f32_16x16x32_bf16 v[30:33], v[218:221], v[186:189], v[30:33]
	v_mfma_f32_16x16x32_bf16 v[22:25], v[210:213], v[194:197], v[22:25]
	v_mfma_f32_16x16x32_bf16 v[14:17], v[218:221], v[194:197], v[14:17]
	v_mfma_f32_16x16x32_bf16 v[6:9], v[210:213], v[202:205], v[6:9]
	v_mfma_f32_16x16x32_bf16 v[2:5], v[218:221], v[202:205], v[2:5]
	s_setprio 0
	s_add_i32 s56, 0, 0x18000
	v_add_u32_e32 v161, s56, v156
	s_barrier
	ds_read_b128 v[142:145], v161
	ds_read_b128 v[162:165], v161 offset:1024
	ds_read_b128 v[166:169], v161 offset:2048
	ds_read_b128 v[170:173], v161 offset:3072
	s_add_u32 s28, s28, 0x40000
	s_addc_u32 s29, s29, 0
	s_mov_b32 m0, s41
	v_lshl_add_u64 v[206:207], s[28:29], 0, v[130:131]
	ds_read_b128 v[174:177], v159 offset:32768
	ds_read_b128 v[178:181], v159 offset:33792
	ds_read_b128 v[182:185], v159 offset:34816
	ds_read_b128 v[186:189], v159 offset:35840
	ds_read_b128 v[190:193], v159 offset:36864
	ds_read_b128 v[194:197], v159 offset:37888
	ds_read_b128 v[198:201], v159 offset:38912
	ds_read_b128 v[202:205], v159 offset:39936
	global_load_lds_dwordx4 v[206:207], off
	v_lshl_add_u64 v[206:207], s[28:29], 0, v[132:133]
	s_mov_b32 m0, s42
	s_nop 0
	global_load_lds_dwordx4 v[206:207], off
	s_waitcnt lgkmcnt(8)
	s_barrier
	s_waitcnt lgkmcnt(0)
	s_setprio 1
	s_waitcnt lgkmcnt(0)
	v_mfma_f32_16x16x32_bf16 v[126:129], v[142:145], v[174:177], v[126:129]
	v_mfma_f32_16x16x32_bf16 v[122:125], v[166:169], v[174:177], v[122:125]
	v_mfma_f32_16x16x32_bf16 v[114:117], v[142:145], v[182:185], v[114:117]
	v_mfma_f32_16x16x32_bf16 v[106:109], v[166:169], v[182:185], v[106:109]
	v_mfma_f32_16x16x32_bf16 v[98:101], v[142:145], v[190:193], v[98:101]
	v_mfma_f32_16x16x32_bf16 v[90:93], v[166:169], v[190:193], v[90:93]
	v_mfma_f32_16x16x32_bf16 v[82:85], v[142:145], v[198:201], v[82:85]
	v_mfma_f32_16x16x32_bf16 v[74:77], v[166:169], v[198:201], v[74:77]
	v_mfma_f32_16x16x32_bf16 v[126:129], v[162:165], v[178:181], v[126:129]
	v_mfma_f32_16x16x32_bf16 v[122:125], v[170:173], v[178:181], v[122:125]
	v_mfma_f32_16x16x32_bf16 v[114:117], v[162:165], v[186:189], v[114:117]
	v_mfma_f32_16x16x32_bf16 v[106:109], v[170:173], v[186:189], v[106:109]
	v_mfma_f32_16x16x32_bf16 v[98:101], v[162:165], v[194:197], v[98:101]
	v_mfma_f32_16x16x32_bf16 v[90:93], v[170:173], v[194:197], v[90:93]
	v_mfma_f32_16x16x32_bf16 v[82:85], v[162:165], v[202:205], v[82:85]
	v_mfma_f32_16x16x32_bf16 v[74:77], v[170:173], v[202:205], v[74:77]
	s_setprio 0
	s_barrier
	s_add_i32 s28, 0, 0x1c000
	s_add_i32 s29, s56, s38
	v_add_u32_e32 v161, s28, v156
	v_lshl_add_u64 v[146:147], v[146:147], 0, s[8:9]
	s_mov_b32 m0, s29
	ds_read_b128 v[206:209], v161
	ds_read_b128 v[210:213], v161 offset:1024
	ds_read_b128 v[214:217], v161 offset:2048
	ds_read_b128 v[218:221], v161 offset:3072
	global_load_lds_dwordx4 v[146:147], off
	v_lshl_add_u64 v[146:147], v[222:223], 0, s[8:9]
	s_add_i32 m0, s29, 0x2000
	s_nop 0
	global_load_lds_dwordx4 v[146:147], off
	s_barrier
	s_waitcnt lgkmcnt(0)
	s_setprio 1
	s_waitcnt lgkmcnt(0)
	v_mfma_f32_16x16x32_bf16 v[118:121], v[206:209], v[174:177], v[118:121]
	v_mfma_f32_16x16x32_bf16 v[110:113], v[214:217], v[174:177], v[110:113]
	v_mfma_f32_16x16x32_bf16 v[102:105], v[206:209], v[182:185], v[102:105]
	v_mfma_f32_16x16x32_bf16 v[94:97], v[214:217], v[182:185], v[94:97]
	v_mfma_f32_16x16x32_bf16 v[86:89], v[206:209], v[190:193], v[86:89]
	v_mfma_f32_16x16x32_bf16 v[78:81], v[214:217], v[190:193], v[78:81]
	v_mfma_f32_16x16x32_bf16 v[70:73], v[206:209], v[198:201], v[70:73]
	v_mfma_f32_16x16x32_bf16 v[66:69], v[214:217], v[198:201], v[66:69]
	v_mfma_f32_16x16x32_bf16 v[118:121], v[210:213], v[178:181], v[118:121]
	v_mfma_f32_16x16x32_bf16 v[110:113], v[218:221], v[178:181], v[110:113]
	v_mfma_f32_16x16x32_bf16 v[102:105], v[210:213], v[186:189], v[102:105]
	v_mfma_f32_16x16x32_bf16 v[94:97], v[218:221], v[186:189], v[94:97]
	v_mfma_f32_16x16x32_bf16 v[86:89], v[210:213], v[194:197], v[86:89]
	v_mfma_f32_16x16x32_bf16 v[78:81], v[218:221], v[194:197], v[78:81]
	v_mfma_f32_16x16x32_bf16 v[70:73], v[210:213], v[202:205], v[70:73]
	v_mfma_f32_16x16x32_bf16 v[66:69], v[218:221], v[202:205], v[66:69]
	s_setprio 0
	s_mov_b32 m0, s44
	v_lshl_add_u64 v[146:147], v[224:225], 0, s[8:9]
	s_barrier
	ds_read_b128 v[174:177], v159 offset:49152
	ds_read_b128 v[178:181], v159 offset:50176
	ds_read_b128 v[182:185], v159 offset:51200
	ds_read_b128 v[186:189], v159 offset:52224
	ds_read_b128 v[190:193], v159 offset:53248
	ds_read_b128 v[194:197], v159 offset:54272
	ds_read_b128 v[198:201], v159 offset:55296
	ds_read_b128 v[202:205], v159 offset:56320
	global_load_lds_dwordx4 v[146:147], off
	v_lshl_add_u64 v[146:147], v[226:227], 0, s[8:9]
	s_mov_b32 m0, s45
	s_nop 0
	global_load_lds_dwordx4 v[146:147], off
	s_barrier
	s_waitcnt lgkmcnt(0)
	s_setprio 1
	s_waitcnt lgkmcnt(0)
	v_mfma_f32_16x16x32_bf16 v[62:65], v[142:145], v[174:177], v[62:65]
	v_mfma_f32_16x16x32_bf16 v[58:61], v[166:169], v[174:177], v[58:61]
	v_mfma_f32_16x16x32_bf16 v[50:53], v[142:145], v[182:185], v[50:53]
	v_mfma_f32_16x16x32_bf16 v[42:45], v[166:169], v[182:185], v[42:45]
	v_mfma_f32_16x16x32_bf16 v[34:37], v[142:145], v[190:193], v[34:37]
	v_mfma_f32_16x16x32_bf16 v[26:29], v[166:169], v[190:193], v[26:29]
	v_mfma_f32_16x16x32_bf16 v[18:21], v[142:145], v[198:201], v[18:21]
	v_mfma_f32_16x16x32_bf16 v[10:13], v[166:169], v[198:201], v[10:13]
	v_mfma_f32_16x16x32_bf16 v[62:65], v[162:165], v[178:181], v[62:65]
	v_mfma_f32_16x16x32_bf16 v[58:61], v[170:173], v[178:181], v[58:61]
	v_mfma_f32_16x16x32_bf16 v[50:53], v[162:165], v[186:189], v[50:53]
	v_mfma_f32_16x16x32_bf16 v[42:45], v[170:173], v[186:189], v[42:45]
	v_mfma_f32_16x16x32_bf16 v[34:37], v[162:165], v[194:197], v[34:37]
	v_mfma_f32_16x16x32_bf16 v[26:29], v[170:173], v[194:197], v[26:29]
	v_mfma_f32_16x16x32_bf16 v[18:21], v[162:165], v[202:205], v[18:21]
	v_mfma_f32_16x16x32_bf16 v[10:13], v[170:173], v[202:205], v[10:13]
	s_setprio 0
	s_barrier
	s_add_u32 s26, s26, 0x40080
	s_addc_u32 s27, s27, 0
	s_add_i32 s28, s28, s38
	v_lshl_add_u64 v[142:143], s[26:27], 0, v[130:131]
	s_mov_b32 m0, s28
	s_nop 0
	global_load_lds_dwordx4 v[142:143], off
	v_lshl_add_u64 v[142:143], s[26:27], 0, v[132:133]
	s_add_i32 m0, s28, 0x2000
	s_nop 0
	global_load_lds_dwordx4 v[142:143], off
	s_waitcnt vmcnt(6)
	s_barrier
	s_setprio 1
	v_mfma_f32_16x16x32_bf16 v[54:57], v[206:209], v[174:177], v[54:57]
	v_mfma_f32_16x16x32_bf16 v[46:49], v[214:217], v[174:177], v[46:49]
	v_mfma_f32_16x16x32_bf16 v[38:41], v[206:209], v[182:185], v[38:41]
	v_mfma_f32_16x16x32_bf16 v[30:33], v[214:217], v[182:185], v[30:33]
	v_mfma_f32_16x16x32_bf16 v[22:25], v[206:209], v[190:193], v[22:25]
	v_mfma_f32_16x16x32_bf16 v[14:17], v[214:217], v[190:193], v[14:17]
	v_mfma_f32_16x16x32_bf16 v[6:9], v[206:209], v[198:201], v[6:9]
	v_mfma_f32_16x16x32_bf16 v[2:5], v[214:217], v[198:201], v[2:5]
	v_mfma_f32_16x16x32_bf16 v[54:57], v[210:213], v[178:181], v[54:57]
	v_mfma_f32_16x16x32_bf16 v[46:49], v[218:221], v[178:181], v[46:49]
	v_mfma_f32_16x16x32_bf16 v[38:41], v[210:213], v[186:189], v[38:41]
	v_mfma_f32_16x16x32_bf16 v[30:33], v[218:221], v[186:189], v[30:33]
	v_mfma_f32_16x16x32_bf16 v[22:25], v[210:213], v[194:197], v[22:25]
	v_mfma_f32_16x16x32_bf16 v[14:17], v[218:221], v[194:197], v[14:17]
	v_mfma_f32_16x16x32_bf16 v[6:9], v[210:213], v[202:205], v[6:9]
	v_mfma_f32_16x16x32_bf16 v[2:5], v[218:221], v[202:205], v[2:5]
	s_setprio 0
	s_add_i32 s55, s55, 2
	s_add_u32 s24, s24, 0x100
	s_addc_u32 s25, s25, 0
	s_add_u32 s53, s53, 0x100
	s_addc_u32 s54, s54, 0
	s_cmp_gt_u32 s55, 13
	s_barrier
	s_cbranch_scc0 .LBB0_3231
	v_lshl_or_b32 v142, s50, 8, v157
	v_lshl_add_u32 v144, s22, 8, v155
	v_ashrrev_i32_e32 v143, 31, v142
	v_mov_b64_e32 v[146:147], s[10:11]
	v_mad_i64_i32 v[162:163], s[24:25], v144, s49, v[146:147]
	v_lshlrev_b64 v[142:143], 1, v[142:143]
	v_lshl_add_u64 v[162:163], v[162:163], 0, v[142:143]
	v_mov_b32_e32 v238, v162
	v_mov_b32_e32 v239, v163
	global_load_dwordx2 v[168:169], v[238:239], off
	global_load_dwordx2 v[170:171], v[238:239], off offset:32
	global_load_dwordx2 v[172:173], v[238:239], off offset:256
	global_load_dwordx2 v[174:175], v[238:239], off offset:288
	v_mov_b32_e32 v242, 16
	v_mad_i64_i32 v[240:241], s[24:25], v242, s49, v[238:239]
	global_load_dwordx2 v[176:177], v[240:241], off
	global_load_dwordx2 v[178:179], v[240:241], off offset:32
	global_load_dwordx2 v[180:181], v[240:241], off offset:256
	global_load_dwordx2 v[182:183], v[240:241], off offset:288
	v_mov_b32_e32 v242, 32
	v_mad_i64_i32 v[240:241], s[24:25], v242, s49, v[238:239]
	global_load_dwordx2 v[184:185], v[240:241], off
	global_load_dwordx2 v[186:187], v[240:241], off offset:32
	global_load_dwordx2 v[188:189], v[240:241], off offset:256
	global_load_dwordx2 v[190:191], v[240:241], off offset:288
	v_mov_b32_e32 v242, 48
	v_mad_i64_i32 v[240:241], s[24:25], v242, s49, v[238:239]
	global_load_dwordx2 v[192:193], v[240:241], off
	global_load_dwordx2 v[194:195], v[240:241], off offset:32
	global_load_dwordx2 v[196:197], v[240:241], off offset:256
	global_load_dwordx2 v[198:199], v[240:241], off offset:288
	v_mov_b32_e32 v242, 128
	v_mad_i64_i32 v[240:241], s[24:25], v242, s49, v[238:239]
	global_load_dwordx2 v[200:201], v[240:241], off
	global_load_dwordx2 v[202:203], v[240:241], off offset:32
	global_load_dwordx2 v[204:205], v[240:241], off offset:256
	global_load_dwordx2 v[206:207], v[240:241], off offset:288
	v_mov_b32_e32 v242, 144
	v_mad_i64_i32 v[240:241], s[24:25], v242, s49, v[238:239]
	global_load_dwordx2 v[208:209], v[240:241], off
	global_load_dwordx2 v[210:211], v[240:241], off offset:32
	global_load_dwordx2 v[212:213], v[240:241], off offset:256
	global_load_dwordx2 v[214:215], v[240:241], off offset:288
	v_mov_b32_e32 v242, 160
	v_mad_i64_i32 v[240:241], s[24:25], v242, s49, v[238:239]
	global_load_dwordx2 v[216:217], v[240:241], off
	global_load_dwordx2 v[218:219], v[240:241], off offset:32
	global_load_dwordx2 v[220:221], v[240:241], off offset:256
	global_load_dwordx2 v[228:229], v[240:241], off offset:288
	v_mov_b32_e32 v242, 176
	v_mad_i64_i32 v[240:241], s[24:25], v242, s49, v[238:239]
	global_load_dwordx2 v[230:231], v[240:241], off
	global_load_dwordx2 v[232:233], v[240:241], off offset:32
	global_load_dwordx2 v[234:235], v[240:241], off offset:256
	global_load_dwordx2 v[236:237], v[240:241], off offset:288
	s_waitcnt vmcnt(0)
	v_mov_b32_e32 v164, v168
	v_mov_b32_e32 v165, v169
	v_ashrrev_i32_e32 v145, 31, v144
	s_and_b64 vcc, exec, s[0:1]
	s_mov_b32 s50, s14
	s_mov_b32 s22, s16
	s_mov_b64 s[26:27], s[20:21]
	s_nop 0
	v_lshlrev_b32_e32 v166, 16, v164
	v_and_b32_e32 v167, 0xffff0000, v164
	v_lshlrev_b32_e32 v164, 16, v165
	v_and_b32_e32 v165, 0xffff0000, v165
	v_pk_mul_f32 v[128:129], v[128:129], v[164:165]
	v_pk_mul_f32 v[126:127], v[126:127], v[166:167]
	v_lshlrev_b64 v[164:165], 12, v[144:145]
	v_cvt_pk_bf16_f32 v126, v126, v127
	v_cvt_pk_bf16_f32 v127, v128, v129
	v_mov_b32_e32 v128, v170
	v_mov_b32_e32 v129, v171
	v_lshl_add_u64 v[164:165], s[12:13], 0, v[164:165]
	v_lshl_add_u64 v[164:165], v[164:165], 0, v[142:143]
	global_store_dwordx2 v[164:165], v[126:127], off
	s_nop 0
	v_lshlrev_b32_e32 v126, 16, v128
	v_and_b32_e32 v127, 0xffff0000, v128
	v_lshlrev_b32_e32 v128, 16, v129
	v_and_b32_e32 v129, 0xffff0000, v129
	v_pk_mul_f32 v[124:125], v[124:125], v[128:129]
	v_pk_mul_f32 v[122:123], v[122:123], v[126:127]
	s_nop 0
	v_cvt_pk_bf16_f32 v122, v122, v123
	v_cvt_pk_bf16_f32 v123, v124, v125
	v_mov_b32_e32 v124, v172
	v_mov_b32_e32 v125, v173
	s_nop 0
	global_store_dwordx2 v[164:165], v[122:123], off offset:32
	s_nop 0
	v_lshlrev_b32_e32 v122, 16, v124
	v_and_b32_e32 v123, 0xffff0000, v124
	v_lshlrev_b32_e32 v124, 16, v125
	v_and_b32_e32 v125, 0xffff0000, v125
	v_pk_mul_f32 v[120:121], v[120:121], v[124:125]
	v_pk_mul_f32 v[118:119], v[118:119], v[122:123]
	v_or_b32_e32 v122, 16, v144
	v_cvt_pk_bf16_f32 v118, v118, v119
	v_cvt_pk_bf16_f32 v119, v120, v121
	v_mov_b32_e32 v120, v174
	v_mov_b32_e32 v121, v175
	v_mad_i64_i32 v[124:125], s[24:25], v122, s49, v[146:147]
	global_store_dwordx2 v[164:165], v[118:119], off offset:256
	v_lshl_add_u64 v[124:125], v[124:125], 0, v[142:143]
	v_ashrrev_i32_e32 v123, 31, v122
	s_nop 0
	v_lshlrev_b32_e32 v118, 16, v120
	v_and_b32_e32 v119, 0xffff0000, v120
	v_lshlrev_b32_e32 v120, 16, v121
	v_and_b32_e32 v121, 0xffff0000, v121
	v_pk_mul_f32 v[112:113], v[112:113], v[120:121]
	v_pk_mul_f32 v[110:111], v[110:111], v[118:119]
	s_nop 0
	v_cvt_pk_bf16_f32 v110, v110, v111
	v_cvt_pk_bf16_f32 v111, v112, v113
	v_mov_b32_e32 v112, v176
	v_mov_b32_e32 v113, v177
	s_nop 0
	global_store_dwordx2 v[164:165], v[110:111], off offset:288
	s_nop 0
	v_lshlrev_b32_e32 v110, 16, v112
	v_and_b32_e32 v111, 0xffff0000, v112
	v_lshlrev_b32_e32 v112, 16, v113
	v_and_b32_e32 v113, 0xffff0000, v113
	v_pk_mul_f32 v[112:113], v[116:117], v[112:113]
	v_pk_mul_f32 v[110:111], v[114:115], v[110:111]
	v_lshlrev_b64 v[114:115], 12, v[122:123]
	v_cvt_pk_bf16_f32 v110, v110, v111
	v_cvt_pk_bf16_f32 v111, v112, v113
	v_mov_b32_e32 v112, v178
	v_mov_b32_e32 v113, v179
	v_lshl_add_u64 v[114:115], s[12:13], 0, v[114:115]
	v_lshl_add_u64 v[114:115], v[114:115], 0, v[142:143]
	global_store_dwordx2 v[114:115], v[110:111], off
	s_nop 0
	v_lshlrev_b32_e32 v110, 16, v112
	v_and_b32_e32 v111, 0xffff0000, v112
	v_lshlrev_b32_e32 v112, 16, v113
	v_and_b32_e32 v113, 0xffff0000, v113
	v_pk_mul_f32 v[108:109], v[108:109], v[112:113]
	v_pk_mul_f32 v[106:107], v[106:107], v[110:111]
	s_nop 0
	v_cvt_pk_bf16_f32 v106, v106, v107
	v_cvt_pk_bf16_f32 v107, v108, v109
	v_mov_b32_e32 v108, v180
	v_mov_b32_e32 v109, v181
	s_nop 0
	global_store_dwordx2 v[114:115], v[106:107], off offset:32
	s_nop 0
	v_lshlrev_b32_e32 v106, 16, v108
	v_and_b32_e32 v107, 0xffff0000, v108
	v_lshlrev_b32_e32 v108, 16, v109
	v_and_b32_e32 v109, 0xffff0000, v109
	v_pk_mul_f32 v[104:105], v[104:105], v[108:109]
	v_pk_mul_f32 v[102:103], v[102:103], v[106:107]
	v_or_b32_e32 v106, 32, v144
	v_cvt_pk_bf16_f32 v102, v102, v103
	v_cvt_pk_bf16_f32 v103, v104, v105
	v_mov_b32_e32 v104, v182
	v_mov_b32_e32 v105, v183
	v_mad_i64_i32 v[108:109], s[24:25], v106, s49, v[146:147]
	global_store_dwordx2 v[114:115], v[102:103], off offset:256
	v_lshl_add_u64 v[108:109], v[108:109], 0, v[142:143]
	v_ashrrev_i32_e32 v107, 31, v106
	s_nop 0
	v_lshlrev_b32_e32 v102, 16, v104
	v_and_b32_e32 v103, 0xffff0000, v104
	v_lshlrev_b32_e32 v104, 16, v105
	v_and_b32_e32 v105, 0xffff0000, v105
	v_pk_mul_f32 v[96:97], v[96:97], v[104:105]
	v_pk_mul_f32 v[94:95], v[94:95], v[102:103]
	s_nop 0
	v_cvt_pk_bf16_f32 v94, v94, v95
	v_cvt_pk_bf16_f32 v95, v96, v97
	v_mov_b32_e32 v96, v184
	v_mov_b32_e32 v97, v185
	s_nop 0
	global_store_dwordx2 v[114:115], v[94:95], off offset:288
	s_nop 0
	v_lshlrev_b32_e32 v94, 16, v96
	v_and_b32_e32 v95, 0xffff0000, v96
	v_lshlrev_b32_e32 v96, 16, v97
	v_and_b32_e32 v97, 0xffff0000, v97
	v_pk_mul_f32 v[96:97], v[100:101], v[96:97]
	v_pk_mul_f32 v[94:95], v[98:99], v[94:95]
	v_lshlrev_b64 v[98:99], 12, v[106:107]
	v_cvt_pk_bf16_f32 v94, v94, v95
	v_cvt_pk_bf16_f32 v95, v96, v97
	v_mov_b32_e32 v96, v186
	v_mov_b32_e32 v97, v187
	v_lshl_add_u64 v[98:99], s[12:13], 0, v[98:99]
	v_lshl_add_u64 v[98:99], v[98:99], 0, v[142:143]
	global_store_dwordx2 v[98:99], v[94:95], off
	s_nop 0
	v_lshlrev_b32_e32 v94, 16, v96
	v_and_b32_e32 v95, 0xffff0000, v96
	v_lshlrev_b32_e32 v96, 16, v97
	v_and_b32_e32 v97, 0xffff0000, v97
	v_pk_mul_f32 v[92:93], v[92:93], v[96:97]
	v_pk_mul_f32 v[90:91], v[90:91], v[94:95]
	s_nop 0
	v_cvt_pk_bf16_f32 v90, v90, v91
	v_cvt_pk_bf16_f32 v91, v92, v93
	v_mov_b32_e32 v92, v188
	v_mov_b32_e32 v93, v189
	s_nop 0
	global_store_dwordx2 v[98:99], v[90:91], off offset:32
	s_nop 0
	v_lshlrev_b32_e32 v90, 16, v92
	v_and_b32_e32 v91, 0xffff0000, v92
	v_lshlrev_b32_e32 v92, 16, v93
	v_and_b32_e32 v93, 0xffff0000, v93
	v_pk_mul_f32 v[88:89], v[88:89], v[92:93]
	v_pk_mul_f32 v[86:87], v[86:87], v[90:91]
	v_or_b32_e32 v90, 48, v144
	v_cvt_pk_bf16_f32 v86, v86, v87
	v_cvt_pk_bf16_f32 v87, v88, v89
	v_mov_b32_e32 v88, v190
	v_mov_b32_e32 v89, v191
	v_mad_i64_i32 v[92:93], s[24:25], v90, s49, v[146:147]
	global_store_dwordx2 v[98:99], v[86:87], off offset:256
	v_lshl_add_u64 v[92:93], v[92:93], 0, v[142:143]
	v_ashrrev_i32_e32 v91, 31, v90
	s_nop 0
	v_lshlrev_b32_e32 v86, 16, v88
	v_and_b32_e32 v87, 0xffff0000, v88
	v_lshlrev_b32_e32 v88, 16, v89
	v_and_b32_e32 v89, 0xffff0000, v89
	v_pk_mul_f32 v[80:81], v[80:81], v[88:89]
	v_pk_mul_f32 v[78:79], v[78:79], v[86:87]
	s_nop 0
	v_cvt_pk_bf16_f32 v78, v78, v79
	v_cvt_pk_bf16_f32 v79, v80, v81
	v_mov_b32_e32 v80, v192
	v_mov_b32_e32 v81, v193
	s_nop 0
	global_store_dwordx2 v[98:99], v[78:79], off offset:288
	s_nop 0
	v_lshlrev_b32_e32 v78, 16, v80
	v_and_b32_e32 v79, 0xffff0000, v80
	v_lshlrev_b32_e32 v80, 16, v81
	v_and_b32_e32 v81, 0xffff0000, v81
	v_pk_mul_f32 v[80:81], v[84:85], v[80:81]
	v_pk_mul_f32 v[78:79], v[82:83], v[78:79]
	v_lshlrev_b64 v[82:83], 12, v[90:91]
	v_cvt_pk_bf16_f32 v78, v78, v79
	v_cvt_pk_bf16_f32 v79, v80, v81
	v_mov_b32_e32 v80, v194
	v_mov_b32_e32 v81, v195
	v_lshl_add_u64 v[82:83], s[12:13], 0, v[82:83]
	v_lshl_add_u64 v[82:83], v[82:83], 0, v[142:143]
	global_store_dwordx2 v[82:83], v[78:79], off
	s_nop 0
	v_lshlrev_b32_e32 v78, 16, v80
	v_and_b32_e32 v79, 0xffff0000, v80
	v_lshlrev_b32_e32 v80, 16, v81
	v_and_b32_e32 v81, 0xffff0000, v81
	v_pk_mul_f32 v[76:77], v[76:77], v[80:81]
	v_pk_mul_f32 v[74:75], v[74:75], v[78:79]
	s_nop 0
	v_cvt_pk_bf16_f32 v74, v74, v75
	v_cvt_pk_bf16_f32 v75, v76, v77
	v_mov_b32_e32 v76, v196
	v_mov_b32_e32 v77, v197
	s_nop 0
	global_store_dwordx2 v[82:83], v[74:75], off offset:32
	s_nop 0
	v_lshlrev_b32_e32 v74, 16, v76
	v_and_b32_e32 v75, 0xffff0000, v76
	v_lshlrev_b32_e32 v76, 16, v77
	v_and_b32_e32 v77, 0xffff0000, v77
	v_pk_mul_f32 v[72:73], v[72:73], v[76:77]
	v_pk_mul_f32 v[70:71], v[70:71], v[74:75]
	v_add_u32_e32 v74, 0x80, v144
	v_cvt_pk_bf16_f32 v70, v70, v71
	v_cvt_pk_bf16_f32 v71, v72, v73
	v_mov_b32_e32 v72, v198
	v_mov_b32_e32 v73, v199
	v_mad_i64_i32 v[76:77], s[24:25], v74, s49, v[146:147]
	global_store_dwordx2 v[82:83], v[70:71], off offset:256
	v_lshl_add_u64 v[76:77], v[76:77], 0, v[142:143]
	v_ashrrev_i32_e32 v75, 31, v74
	s_nop 0
	v_lshlrev_b32_e32 v70, 16, v72
	v_and_b32_e32 v71, 0xffff0000, v72
	v_lshlrev_b32_e32 v72, 16, v73
	v_and_b32_e32 v73, 0xffff0000, v73
	v_pk_mul_f32 v[68:69], v[68:69], v[72:73]
	v_pk_mul_f32 v[66:67], v[66:67], v[70:71]
	s_nop 0
	v_cvt_pk_bf16_f32 v66, v66, v67
	v_cvt_pk_bf16_f32 v67, v68, v69
	v_mov_b32_e32 v68, v200
	v_mov_b32_e32 v69, v201
	s_nop 0
	global_store_dwordx2 v[82:83], v[66:67], off offset:288
	s_nop 0
	v_lshlrev_b32_e32 v66, 16, v68
	v_and_b32_e32 v67, 0xffff0000, v68
	v_lshlrev_b32_e32 v68, 16, v69
	v_and_b32_e32 v69, 0xffff0000, v69
	v_pk_mul_f32 v[64:65], v[64:65], v[68:69]
	v_pk_mul_f32 v[62:63], v[62:63], v[66:67]
	v_lshlrev_b64 v[66:67], 12, v[74:75]
	v_cvt_pk_bf16_f32 v62, v62, v63
	v_cvt_pk_bf16_f32 v63, v64, v65
	v_mov_b32_e32 v64, v202
	v_mov_b32_e32 v65, v203
	v_lshl_add_u64 v[66:67], s[12:13], 0, v[66:67]
	v_lshl_add_u64 v[66:67], v[66:67], 0, v[142:143]
	global_store_dwordx2 v[66:67], v[62:63], off
	s_nop 0
	v_lshlrev_b32_e32 v62, 16, v64
	v_and_b32_e32 v63, 0xffff0000, v64
	v_lshlrev_b32_e32 v64, 16, v65
	v_and_b32_e32 v65, 0xffff0000, v65
	v_pk_mul_f32 v[60:61], v[60:61], v[64:65]
	v_pk_mul_f32 v[58:59], v[58:59], v[62:63]
	s_nop 0
	v_cvt_pk_bf16_f32 v58, v58, v59
	v_cvt_pk_bf16_f32 v59, v60, v61
	v_mov_b32_e32 v60, v204
	v_mov_b32_e32 v61, v205
	s_nop 0
	global_store_dwordx2 v[66:67], v[58:59], off offset:32
	s_nop 0
	v_lshlrev_b32_e32 v58, 16, v60
	v_and_b32_e32 v59, 0xffff0000, v60
	v_lshlrev_b32_e32 v60, 16, v61
	v_and_b32_e32 v61, 0xffff0000, v61
	v_pk_mul_f32 v[56:57], v[56:57], v[60:61]
	v_pk_mul_f32 v[54:55], v[54:55], v[58:59]
	v_add_u32_e32 v58, 0x90, v144
	v_cvt_pk_bf16_f32 v54, v54, v55
	v_cvt_pk_bf16_f32 v55, v56, v57
	v_mov_b32_e32 v56, v206
	v_mov_b32_e32 v57, v207
	v_mad_i64_i32 v[60:61], s[24:25], v58, s49, v[146:147]
	global_store_dwordx2 v[66:67], v[54:55], off offset:256
	v_lshl_add_u64 v[60:61], v[60:61], 0, v[142:143]
	v_ashrrev_i32_e32 v59, 31, v58
	s_nop 0
	v_lshlrev_b32_e32 v54, 16, v56
	v_and_b32_e32 v55, 0xffff0000, v56
	v_lshlrev_b32_e32 v56, 16, v57
	v_and_b32_e32 v57, 0xffff0000, v57
	v_pk_mul_f32 v[48:49], v[48:49], v[56:57]
	v_pk_mul_f32 v[46:47], v[46:47], v[54:55]
	s_nop 0
	v_cvt_pk_bf16_f32 v46, v46, v47
	v_cvt_pk_bf16_f32 v47, v48, v49
	v_mov_b32_e32 v48, v208
	v_mov_b32_e32 v49, v209
	s_nop 0
	global_store_dwordx2 v[66:67], v[46:47], off offset:288
	s_nop 0
	v_lshlrev_b32_e32 v46, 16, v48
	v_and_b32_e32 v47, 0xffff0000, v48
	v_lshlrev_b32_e32 v48, 16, v49
	v_and_b32_e32 v49, 0xffff0000, v49
	v_pk_mul_f32 v[48:49], v[52:53], v[48:49]
	v_pk_mul_f32 v[46:47], v[50:51], v[46:47]
	v_lshlrev_b64 v[50:51], 12, v[58:59]
	v_cvt_pk_bf16_f32 v46, v46, v47
	v_cvt_pk_bf16_f32 v47, v48, v49
	v_mov_b32_e32 v48, v210
	v_mov_b32_e32 v49, v211
	v_lshl_add_u64 v[50:51], s[12:13], 0, v[50:51]
	v_lshl_add_u64 v[50:51], v[50:51], 0, v[142:143]
	global_store_dwordx2 v[50:51], v[46:47], off
	s_nop 0
	v_lshlrev_b32_e32 v46, 16, v48
	v_and_b32_e32 v47, 0xffff0000, v48
	v_lshlrev_b32_e32 v48, 16, v49
	v_and_b32_e32 v49, 0xffff0000, v49
	v_pk_mul_f32 v[44:45], v[44:45], v[48:49]
	v_pk_mul_f32 v[42:43], v[42:43], v[46:47]
	s_nop 0
	v_cvt_pk_bf16_f32 v42, v42, v43
	v_cvt_pk_bf16_f32 v43, v44, v45
	v_mov_b32_e32 v44, v212
	v_mov_b32_e32 v45, v213
	s_nop 0
	global_store_dwordx2 v[50:51], v[42:43], off offset:32
	s_nop 0
	v_lshlrev_b32_e32 v42, 16, v44
	v_and_b32_e32 v43, 0xffff0000, v44
	v_lshlrev_b32_e32 v44, 16, v45
	v_and_b32_e32 v45, 0xffff0000, v45
	v_pk_mul_f32 v[40:41], v[40:41], v[44:45]
	v_pk_mul_f32 v[38:39], v[38:39], v[42:43]
	v_add_u32_e32 v42, 0xa0, v144
	v_cvt_pk_bf16_f32 v38, v38, v39
	v_cvt_pk_bf16_f32 v39, v40, v41
	v_mov_b32_e32 v40, v214
	v_mov_b32_e32 v41, v215
	v_mad_i64_i32 v[44:45], s[24:25], v42, s49, v[146:147]
	global_store_dwordx2 v[50:51], v[38:39], off offset:256
	v_lshl_add_u64 v[44:45], v[44:45], 0, v[142:143]
	v_ashrrev_i32_e32 v43, 31, v42
	s_nop 0
	v_lshlrev_b32_e32 v38, 16, v40
	v_and_b32_e32 v39, 0xffff0000, v40
	v_lshlrev_b32_e32 v40, 16, v41
	v_and_b32_e32 v41, 0xffff0000, v41
	v_pk_mul_f32 v[32:33], v[32:33], v[40:41]
	v_pk_mul_f32 v[30:31], v[30:31], v[38:39]
	s_nop 0
	v_cvt_pk_bf16_f32 v30, v30, v31
	v_cvt_pk_bf16_f32 v31, v32, v33
	v_mov_b32_e32 v32, v216
	v_mov_b32_e32 v33, v217
	s_nop 0
	global_store_dwordx2 v[50:51], v[30:31], off offset:288
	s_nop 0
	v_lshlrev_b32_e32 v30, 16, v32
	v_and_b32_e32 v31, 0xffff0000, v32
	v_lshlrev_b32_e32 v32, 16, v33
	v_and_b32_e32 v33, 0xffff0000, v33
	v_pk_mul_f32 v[32:33], v[36:37], v[32:33]
	v_pk_mul_f32 v[30:31], v[34:35], v[30:31]
	v_lshlrev_b64 v[34:35], 12, v[42:43]
	v_cvt_pk_bf16_f32 v30, v30, v31
	v_cvt_pk_bf16_f32 v31, v32, v33
	v_mov_b32_e32 v32, v218
	v_mov_b32_e32 v33, v219
	v_lshl_add_u64 v[34:35], s[12:13], 0, v[34:35]
	v_lshl_add_u64 v[34:35], v[34:35], 0, v[142:143]
	global_store_dwordx2 v[34:35], v[30:31], off
	s_nop 0
	v_lshlrev_b32_e32 v30, 16, v32
	v_and_b32_e32 v31, 0xffff0000, v32
	v_lshlrev_b32_e32 v32, 16, v33
	v_and_b32_e32 v33, 0xffff0000, v33
	v_pk_mul_f32 v[28:29], v[28:29], v[32:33]
	v_pk_mul_f32 v[26:27], v[26:27], v[30:31]
	s_nop 0
	v_cvt_pk_bf16_f32 v26, v26, v27
	v_cvt_pk_bf16_f32 v27, v28, v29
	v_mov_b32_e32 v28, v220
	v_mov_b32_e32 v29, v221
	s_nop 0
	global_store_dwordx2 v[34:35], v[26:27], off offset:32
	s_nop 0
	v_lshlrev_b32_e32 v26, 16, v28
	v_and_b32_e32 v27, 0xffff0000, v28
	v_lshlrev_b32_e32 v28, 16, v29
	v_and_b32_e32 v29, 0xffff0000, v29
	v_pk_mul_f32 v[24:25], v[24:25], v[28:29]
	v_pk_mul_f32 v[22:23], v[22:23], v[26:27]
	v_add_u32_e32 v26, 0xb0, v144
	v_cvt_pk_bf16_f32 v22, v22, v23
	v_cvt_pk_bf16_f32 v23, v24, v25
	v_mov_b32_e32 v24, v228
	v_mov_b32_e32 v25, v229
	v_mad_i64_i32 v[28:29], s[24:25], v26, s49, v[146:147]
	global_store_dwordx2 v[34:35], v[22:23], off offset:256
	v_lshl_add_u64 v[28:29], v[28:29], 0, v[142:143]
	v_ashrrev_i32_e32 v27, 31, v26
	s_mov_b64 s[24:25], s[18:19]
	s_nop 0
	v_lshlrev_b32_e32 v22, 16, v24
	v_and_b32_e32 v23, 0xffff0000, v24
	v_lshlrev_b32_e32 v24, 16, v25
	v_and_b32_e32 v25, 0xffff0000, v25
	v_pk_mul_f32 v[16:17], v[16:17], v[24:25]
	v_pk_mul_f32 v[14:15], v[14:15], v[22:23]
	s_nop 0
	v_cvt_pk_bf16_f32 v14, v14, v15
	v_cvt_pk_bf16_f32 v15, v16, v17
	v_mov_b32_e32 v16, v230
	v_mov_b32_e32 v17, v231
	s_nop 0
	global_store_dwordx2 v[34:35], v[14:15], off offset:288
	s_nop 0
	v_lshlrev_b32_e32 v14, 16, v16
	v_and_b32_e32 v15, 0xffff0000, v16
	v_lshlrev_b32_e32 v16, 16, v17
	v_and_b32_e32 v17, 0xffff0000, v17
	v_pk_mul_f32 v[16:17], v[20:21], v[16:17]
	v_pk_mul_f32 v[14:15], v[18:19], v[14:15]
	v_lshlrev_b64 v[18:19], 12, v[26:27]
	v_cvt_pk_bf16_f32 v14, v14, v15
	v_cvt_pk_bf16_f32 v15, v16, v17
	v_mov_b32_e32 v16, v232
	v_mov_b32_e32 v17, v233
	v_lshl_add_u64 v[18:19], s[12:13], 0, v[18:19]
	v_lshl_add_u64 v[18:19], v[18:19], 0, v[142:143]
	global_store_dwordx2 v[18:19], v[14:15], off
	s_nop 0
	v_lshlrev_b32_e32 v14, 16, v16
	v_and_b32_e32 v15, 0xffff0000, v16
	v_lshlrev_b32_e32 v16, 16, v17
	v_and_b32_e32 v17, 0xffff0000, v17
	v_pk_mul_f32 v[12:13], v[12:13], v[16:17]
	v_pk_mul_f32 v[10:11], v[10:11], v[14:15]
	s_nop 0
	v_cvt_pk_bf16_f32 v10, v10, v11
	v_cvt_pk_bf16_f32 v11, v12, v13
	v_mov_b32_e32 v12, v234
	v_mov_b32_e32 v13, v235
	s_nop 0
	global_store_dwordx2 v[18:19], v[10:11], off offset:32
	s_nop 0
	v_lshlrev_b32_e32 v10, 16, v12
	v_and_b32_e32 v11, 0xffff0000, v12
	v_lshlrev_b32_e32 v12, 16, v13
	v_and_b32_e32 v13, 0xffff0000, v13
	v_pk_mul_f32 v[8:9], v[8:9], v[12:13]
	v_pk_mul_f32 v[6:7], v[6:7], v[10:11]
	s_nop 0
	v_cvt_pk_bf16_f32 v6, v6, v7
	v_cvt_pk_bf16_f32 v7, v8, v9
	v_mov_b32_e32 v8, v236
	v_mov_b32_e32 v9, v237
	s_nop 0
	global_store_dwordx2 v[18:19], v[6:7], off offset:256
	s_nop 0
	v_lshlrev_b32_e32 v6, 16, v8
	v_and_b32_e32 v7, 0xffff0000, v8
	v_lshlrev_b32_e32 v8, 16, v9
	v_and_b32_e32 v9, 0xffff0000, v9
	v_pk_mul_f32 v[2:3], v[2:3], v[6:7]
	v_pk_mul_f32 v[4:5], v[4:5], v[8:9]
	v_cvt_pk_bf16_f32 v2, v2, v3
	s_nop 0
	v_cvt_pk_bf16_f32 v3, v4, v5
	global_store_dwordx2 v[18:19], v[2:3], off offset:288
	s_cbranch_vccz .LBB0_3228
	s_waitcnt vmcnt(0)
	s_cmpk_gt_u32 s33, 0xff
	s_cbranch_scc1 .LBB0_3235
	s_barrier

.LBB0_3243:
	ds_read_b128 v[142:145], v158
	ds_read_b128 v[162:165], v158 offset:1024
	ds_read_b128 v[166:169], v158 offset:2048
	ds_read_b128 v[170:173], v158 offset:3072
	s_add_u32 s26, s24, 0xfffc0080
	s_addc_u32 s27, s25, -1
	s_cmp_eq_u32 s56, 12
	s_cselect_b32 s29, s17, s27
	s_cselect_b32 s28, s52, s26
	s_cselect_b32 s27, s15, s55
	s_cselect_b32 s26, s53, s54
	v_lshl_add_u64 v[146:147], s[24:25], 0, v[134:135]
	s_add_i32 m0, s23, 0xc000
	ds_read_b128 v[174:177], v159
	ds_read_b128 v[178:181], v159 offset:1024
	ds_read_b128 v[182:185], v159 offset:2048
	ds_read_b128 v[186:189], v159 offset:3072
	ds_read_b128 v[190:193], v159 offset:4096
	ds_read_b128 v[194:197], v159 offset:5120
	ds_read_b128 v[198:201], v159 offset:6144
	ds_read_b128 v[202:205], v159 offset:7168
	global_load_lds_dwordx4 v[146:147], off
	v_lshl_add_u64 v[146:147], s[24:25], 0, v[136:137]
	s_add_i32 m0, s23, 0xe000
	s_nop 0
	global_load_lds_dwordx4 v[146:147], off
	s_waitcnt lgkmcnt(8)
	s_barrier
	s_waitcnt lgkmcnt(0)
	s_setprio 1
	s_waitcnt lgkmcnt(0)
	v_mfma_f32_16x16x32_bf16 v[126:129], v[142:145], v[174:177], v[126:129]
	v_mfma_f32_16x16x32_bf16 v[122:125], v[166:169], v[174:177], v[122:125]
	v_mfma_f32_16x16x32_bf16 v[110:113], v[142:145], v[182:185], v[110:113]
	v_mfma_f32_16x16x32_bf16 v[106:109], v[166:169], v[182:185], v[106:109]
	v_mfma_f32_16x16x32_bf16 v[94:97], v[142:145], v[190:193], v[94:97]
	v_mfma_f32_16x16x32_bf16 v[90:93], v[166:169], v[190:193], v[90:93]
	v_mfma_f32_16x16x32_bf16 v[78:81], v[142:145], v[198:201], v[78:81]
	v_mfma_f32_16x16x32_bf16 v[74:77], v[166:169], v[198:201], v[74:77]
	v_mfma_f32_16x16x32_bf16 v[126:129], v[162:165], v[178:181], v[126:129]
	v_mfma_f32_16x16x32_bf16 v[122:125], v[170:173], v[178:181], v[122:125]
	v_mfma_f32_16x16x32_bf16 v[110:113], v[162:165], v[186:189], v[110:113]
	v_mfma_f32_16x16x32_bf16 v[106:109], v[170:173], v[186:189], v[106:109]
	v_mfma_f32_16x16x32_bf16 v[94:97], v[162:165], v[194:197], v[94:97]
	v_mfma_f32_16x16x32_bf16 v[90:93], v[170:173], v[194:197], v[90:93]
	v_mfma_f32_16x16x32_bf16 v[78:81], v[162:165], v[202:205], v[78:81]
	v_mfma_f32_16x16x32_bf16 v[74:77], v[170:173], v[202:205], v[74:77]
	s_setprio 0
	s_barrier
	s_add_i32 s57, s47, s38
	v_lshl_add_u64 v[146:147], s[26:27], 0, v[130:131]
	s_mov_b32 m0, s57
	ds_read_b128 v[206:209], v160
	ds_read_b128 v[210:213], v160 offset:1024
	ds_read_b128 v[214:217], v160 offset:2048
	ds_read_b128 v[218:221], v160 offset:3072
	global_load_lds_dwordx4 v[146:147], off
	v_lshl_add_u64 v[222:223], s[26:27], 0, v[132:133]
	s_add_i32 m0, s57, 0x2000
	s_nop 0
	global_load_lds_dwordx4 v[222:223], off
	s_barrier
	s_waitcnt lgkmcnt(0)
	s_setprio 1
	s_waitcnt lgkmcnt(0)
	v_mfma_f32_16x16x32_bf16 v[118:121], v[206:209], v[174:177], v[118:121]
	v_mfma_f32_16x16x32_bf16 v[114:117], v[214:217], v[174:177], v[114:117]
	v_mfma_f32_16x16x32_bf16 v[102:105], v[206:209], v[182:185], v[102:105]
	v_mfma_f32_16x16x32_bf16 v[98:101], v[214:217], v[182:185], v[98:101]
	v_mfma_f32_16x16x32_bf16 v[86:89], v[206:209], v[190:193], v[86:89]
	v_mfma_f32_16x16x32_bf16 v[82:85], v[214:217], v[190:193], v[82:85]
	v_mfma_f32_16x16x32_bf16 v[70:73], v[206:209], v[198:201], v[70:73]
	v_mfma_f32_16x16x32_bf16 v[66:69], v[214:217], v[198:201], v[66:69]
	v_mfma_f32_16x16x32_bf16 v[118:121], v[210:213], v[178:181], v[118:121]
	v_mfma_f32_16x16x32_bf16 v[114:117], v[218:221], v[178:181], v[114:117]
	v_mfma_f32_16x16x32_bf16 v[102:105], v[210:213], v[186:189], v[102:105]
	v_mfma_f32_16x16x32_bf16 v[98:101], v[218:221], v[186:189], v[98:101]
	v_mfma_f32_16x16x32_bf16 v[86:89], v[210:213], v[194:197], v[86:89]
	v_mfma_f32_16x16x32_bf16 v[82:85], v[218:221], v[194:197], v[82:85]
	v_mfma_f32_16x16x32_bf16 v[70:73], v[210:213], v[202:205], v[70:73]
	v_mfma_f32_16x16x32_bf16 v[66:69], v[218:221], v[202:205], v[66:69]
	s_setprio 0
	s_mov_b32 m0, s23
	v_lshl_add_u64 v[224:225], s[28:29], 0, v[130:131]
	s_barrier
	ds_read_b128 v[174:177], v159 offset:16384
	ds_read_b128 v[178:181], v159 offset:17408
	ds_read_b128 v[182:185], v159 offset:18432
	ds_read_b128 v[186:189], v159 offset:19456
	ds_read_b128 v[190:193], v159 offset:20480
	ds_read_b128 v[194:197], v159 offset:21504
	ds_read_b128 v[198:201], v159 offset:22528
	ds_read_b128 v[202:205], v159 offset:23552
	global_load_lds_dwordx4 v[224:225], off
	v_lshl_add_u64 v[226:227], s[28:29], 0, v[132:133]
	s_mov_b32 m0, s40
	s_nop 0
	global_load_lds_dwordx4 v[226:227], off
	s_barrier
	s_waitcnt lgkmcnt(0)
	s_setprio 1
	s_waitcnt lgkmcnt(0)
	v_mfma_f32_16x16x32_bf16 v[62:65], v[142:145], v[174:177], v[62:65]
	v_mfma_f32_16x16x32_bf16 v[58:61], v[166:169], v[174:177], v[58:61]
	v_mfma_f32_16x16x32_bf16 v[46:49], v[142:145], v[182:185], v[46:49]
	v_mfma_f32_16x16x32_bf16 v[42:45], v[166:169], v[182:185], v[42:45]
	v_mfma_f32_16x16x32_bf16 v[30:33], v[142:145], v[190:193], v[30:33]
	v_mfma_f32_16x16x32_bf16 v[26:29], v[166:169], v[190:193], v[26:29]
	v_mfma_f32_16x16x32_bf16 v[14:17], v[142:145], v[198:201], v[14:17]
	v_mfma_f32_16x16x32_bf16 v[10:13], v[166:169], v[198:201], v[10:13]
	v_mfma_f32_16x16x32_bf16 v[62:65], v[162:165], v[178:181], v[62:65]
	v_mfma_f32_16x16x32_bf16 v[58:61], v[170:173], v[178:181], v[58:61]
	v_mfma_f32_16x16x32_bf16 v[46:49], v[162:165], v[186:189], v[46:49]
	v_mfma_f32_16x16x32_bf16 v[42:45], v[170:173], v[186:189], v[42:45]
	v_mfma_f32_16x16x32_bf16 v[30:33], v[162:165], v[194:197], v[30:33]
	v_mfma_f32_16x16x32_bf16 v[26:29], v[170:173], v[194:197], v[26:29]
	v_mfma_f32_16x16x32_bf16 v[14:17], v[162:165], v[202:205], v[14:17]
	v_mfma_f32_16x16x32_bf16 v[10:13], v[170:173], v[202:205], v[10:13]
	s_setprio 0
	s_barrier
	s_add_u32 s58, s26, 0x40000
	s_addc_u32 s59, s27, 0
	s_add_i32 s57, s48, s38
	v_lshl_add_u64 v[142:143], s[58:59], 0, v[130:131]
	s_mov_b32 m0, s57
	s_nop 0
	global_load_lds_dwordx4 v[142:143], off
	v_lshl_add_u64 v[142:143], s[58:59], 0, v[132:133]
	s_add_i32 m0, s57, 0x2000
	s_nop 0
	global_load_lds_dwordx4 v[142:143], off
	s_waitcnt vmcnt(6)
	s_barrier
	s_setprio 1
	v_mfma_f32_16x16x32_bf16 v[54:57], v[206:209], v[174:177], v[54:57]
	v_mfma_f32_16x16x32_bf16 v[50:53], v[214:217], v[174:177], v[50:53]
	v_mfma_f32_16x16x32_bf16 v[38:41], v[206:209], v[182:185], v[38:41]
	v_mfma_f32_16x16x32_bf16 v[34:37], v[214:217], v[182:185], v[34:37]
	v_mfma_f32_16x16x32_bf16 v[22:25], v[206:209], v[190:193], v[22:25]
	v_mfma_f32_16x16x32_bf16 v[18:21], v[214:217], v[190:193], v[18:21]
	v_mfma_f32_16x16x32_bf16 v[6:9], v[206:209], v[198:201], v[6:9]
	v_mfma_f32_16x16x32_bf16 v[2:5], v[214:217], v[198:201], v[2:5]
	v_mfma_f32_16x16x32_bf16 v[54:57], v[210:213], v[178:181], v[54:57]
	v_mfma_f32_16x16x32_bf16 v[50:53], v[218:221], v[178:181], v[50:53]
	v_mfma_f32_16x16x32_bf16 v[38:41], v[210:213], v[186:189], v[38:41]
	v_mfma_f32_16x16x32_bf16 v[34:37], v[218:221], v[186:189], v[34:37]
	v_mfma_f32_16x16x32_bf16 v[22:25], v[210:213], v[194:197], v[22:25]
	v_mfma_f32_16x16x32_bf16 v[18:21], v[218:221], v[194:197], v[18:21]
	v_mfma_f32_16x16x32_bf16 v[6:9], v[210:213], v[202:205], v[6:9]
	v_mfma_f32_16x16x32_bf16 v[2:5], v[218:221], v[202:205], v[2:5]
	s_setprio 0
	s_add_i32 s57, 0, 0x18000
	v_add_u32_e32 v161, s57, v156
	s_barrier
	ds_read_b128 v[142:145], v161
	ds_read_b128 v[162:165], v161 offset:1024
	ds_read_b128 v[166:169], v161 offset:2048
	ds_read_b128 v[170:173], v161 offset:3072
	s_add_u32 s28, s28, 0x40000
	s_addc_u32 s29, s29, 0
	s_mov_b32 m0, s41
	v_lshl_add_u64 v[206:207], s[28:29], 0, v[130:131]
	ds_read_b128 v[174:177], v159 offset:32768
	ds_read_b128 v[178:181], v159 offset:33792
	ds_read_b128 v[182:185], v159 offset:34816
	ds_read_b128 v[186:189], v159 offset:35840
	ds_read_b128 v[190:193], v159 offset:36864
	ds_read_b128 v[194:197], v159 offset:37888
	ds_read_b128 v[198:201], v159 offset:38912
	ds_read_b128 v[202:205], v159 offset:39936
	global_load_lds_dwordx4 v[206:207], off
	v_lshl_add_u64 v[206:207], s[28:29], 0, v[132:133]
	s_mov_b32 m0, s42
	s_nop 0
	global_load_lds_dwordx4 v[206:207], off
	s_waitcnt lgkmcnt(8)
	s_barrier
	s_waitcnt lgkmcnt(0)
	s_setprio 1
	s_waitcnt lgkmcnt(0)
	v_mfma_f32_16x16x32_bf16 v[126:129], v[142:145], v[174:177], v[126:129]
	v_mfma_f32_16x16x32_bf16 v[122:125], v[166:169], v[174:177], v[122:125]
	v_mfma_f32_16x16x32_bf16 v[110:113], v[142:145], v[182:185], v[110:113]
	v_mfma_f32_16x16x32_bf16 v[106:109], v[166:169], v[182:185], v[106:109]
	v_mfma_f32_16x16x32_bf16 v[94:97], v[142:145], v[190:193], v[94:97]
	v_mfma_f32_16x16x32_bf16 v[90:93], v[166:169], v[190:193], v[90:93]
	v_mfma_f32_16x16x32_bf16 v[78:81], v[142:145], v[198:201], v[78:81]
	v_mfma_f32_16x16x32_bf16 v[74:77], v[166:169], v[198:201], v[74:77]
	v_mfma_f32_16x16x32_bf16 v[126:129], v[162:165], v[178:181], v[126:129]
	v_mfma_f32_16x16x32_bf16 v[122:125], v[170:173], v[178:181], v[122:125]
	v_mfma_f32_16x16x32_bf16 v[110:113], v[162:165], v[186:189], v[110:113]
	v_mfma_f32_16x16x32_bf16 v[106:109], v[170:173], v[186:189], v[106:109]
	v_mfma_f32_16x16x32_bf16 v[94:97], v[162:165], v[194:197], v[94:97]
	v_mfma_f32_16x16x32_bf16 v[90:93], v[170:173], v[194:197], v[90:93]
	v_mfma_f32_16x16x32_bf16 v[78:81], v[162:165], v[202:205], v[78:81]
	v_mfma_f32_16x16x32_bf16 v[74:77], v[170:173], v[202:205], v[74:77]
	s_setprio 0
	s_barrier
	s_add_i32 s28, 0, 0x1c000
	s_add_i32 s29, s57, s38
	v_add_u32_e32 v161, s28, v156
	v_lshl_add_u64 v[146:147], v[146:147], 0, s[8:9]
	s_mov_b32 m0, s29
	ds_read_b128 v[206:209], v161
	ds_read_b128 v[210:213], v161 offset:1024
	ds_read_b128 v[214:217], v161 offset:2048
	ds_read_b128 v[218:221], v161 offset:3072
	global_load_lds_dwordx4 v[146:147], off
	v_lshl_add_u64 v[146:147], v[222:223], 0, s[8:9]
	s_add_i32 m0, s29, 0x2000
	s_nop 0
	global_load_lds_dwordx4 v[146:147], off
	s_barrier
	s_waitcnt lgkmcnt(0)
	s_setprio 1
	s_waitcnt lgkmcnt(0)
	v_mfma_f32_16x16x32_bf16 v[118:121], v[206:209], v[174:177], v[118:121]
	v_mfma_f32_16x16x32_bf16 v[114:117], v[214:217], v[174:177], v[114:117]
	v_mfma_f32_16x16x32_bf16 v[102:105], v[206:209], v[182:185], v[102:105]
	v_mfma_f32_16x16x32_bf16 v[98:101], v[214:217], v[182:185], v[98:101]
	v_mfma_f32_16x16x32_bf16 v[86:89], v[206:209], v[190:193], v[86:89]
	v_mfma_f32_16x16x32_bf16 v[82:85], v[214:217], v[190:193], v[82:85]
	v_mfma_f32_16x16x32_bf16 v[70:73], v[206:209], v[198:201], v[70:73]
	v_mfma_f32_16x16x32_bf16 v[66:69], v[214:217], v[198:201], v[66:69]
	v_mfma_f32_16x16x32_bf16 v[118:121], v[210:213], v[178:181], v[118:121]
	v_mfma_f32_16x16x32_bf16 v[114:117], v[218:221], v[178:181], v[114:117]
	v_mfma_f32_16x16x32_bf16 v[102:105], v[210:213], v[186:189], v[102:105]
	v_mfma_f32_16x16x32_bf16 v[98:101], v[218:221], v[186:189], v[98:101]
	v_mfma_f32_16x16x32_bf16 v[86:89], v[210:213], v[194:197], v[86:89]
	v_mfma_f32_16x16x32_bf16 v[82:85], v[218:221], v[194:197], v[82:85]
	v_mfma_f32_16x16x32_bf16 v[70:73], v[210:213], v[202:205], v[70:73]
	v_mfma_f32_16x16x32_bf16 v[66:69], v[218:221], v[202:205], v[66:69]
	s_setprio 0
	s_mov_b32 m0, s44
	v_lshl_add_u64 v[146:147], v[224:225], 0, s[8:9]
	s_barrier
	ds_read_b128 v[174:177], v159 offset:49152
	ds_read_b128 v[178:181], v159 offset:50176
	ds_read_b128 v[182:185], v159 offset:51200
	ds_read_b128 v[186:189], v159 offset:52224
	ds_read_b128 v[190:193], v159 offset:53248
	ds_read_b128 v[194:197], v159 offset:54272
	ds_read_b128 v[198:201], v159 offset:55296
	ds_read_b128 v[202:205], v159 offset:56320
	global_load_lds_dwordx4 v[146:147], off
	v_lshl_add_u64 v[146:147], v[226:227], 0, s[8:9]
	s_mov_b32 m0, s45
	s_nop 0
	global_load_lds_dwordx4 v[146:147], off
	s_barrier
	s_waitcnt lgkmcnt(0)
	s_setprio 1
	s_waitcnt lgkmcnt(0)
	v_mfma_f32_16x16x32_bf16 v[62:65], v[142:145], v[174:177], v[62:65]
	v_mfma_f32_16x16x32_bf16 v[58:61], v[166:169], v[174:177], v[58:61]
	v_mfma_f32_16x16x32_bf16 v[46:49], v[142:145], v[182:185], v[46:49]
	v_mfma_f32_16x16x32_bf16 v[42:45], v[166:169], v[182:185], v[42:45]
	v_mfma_f32_16x16x32_bf16 v[30:33], v[142:145], v[190:193], v[30:33]
	v_mfma_f32_16x16x32_bf16 v[26:29], v[166:169], v[190:193], v[26:29]
	v_mfma_f32_16x16x32_bf16 v[14:17], v[142:145], v[198:201], v[14:17]
	v_mfma_f32_16x16x32_bf16 v[10:13], v[166:169], v[198:201], v[10:13]
	v_mfma_f32_16x16x32_bf16 v[62:65], v[162:165], v[178:181], v[62:65]
	v_mfma_f32_16x16x32_bf16 v[58:61], v[170:173], v[178:181], v[58:61]
	v_mfma_f32_16x16x32_bf16 v[46:49], v[162:165], v[186:189], v[46:49]
	v_mfma_f32_16x16x32_bf16 v[42:45], v[170:173], v[186:189], v[42:45]
	v_mfma_f32_16x16x32_bf16 v[30:33], v[162:165], v[194:197], v[30:33]
	v_mfma_f32_16x16x32_bf16 v[26:29], v[170:173], v[194:197], v[26:29]
	v_mfma_f32_16x16x32_bf16 v[14:17], v[162:165], v[202:205], v[14:17]
	v_mfma_f32_16x16x32_bf16 v[10:13], v[170:173], v[202:205], v[10:13]
	s_setprio 0
	s_barrier
	s_add_u32 s26, s26, 0x40080
	s_addc_u32 s27, s27, 0
	s_add_i32 s28, s28, s38
	v_lshl_add_u64 v[142:143], s[26:27], 0, v[130:131]
	s_mov_b32 m0, s28
	s_nop 0
	global_load_lds_dwordx4 v[142:143], off
	v_lshl_add_u64 v[142:143], s[26:27], 0, v[132:133]
	s_add_i32 m0, s28, 0x2000
	s_nop 0
	global_load_lds_dwordx4 v[142:143], off
	s_waitcnt vmcnt(6)
	s_barrier
	s_setprio 1
	v_mfma_f32_16x16x32_bf16 v[54:57], v[206:209], v[174:177], v[54:57]
	v_mfma_f32_16x16x32_bf16 v[50:53], v[214:217], v[174:177], v[50:53]
	v_mfma_f32_16x16x32_bf16 v[38:41], v[206:209], v[182:185], v[38:41]
	v_mfma_f32_16x16x32_bf16 v[34:37], v[214:217], v[182:185], v[34:37]
	v_mfma_f32_16x16x32_bf16 v[22:25], v[206:209], v[190:193], v[22:25]
	v_mfma_f32_16x16x32_bf16 v[18:21], v[214:217], v[190:193], v[18:21]
	v_mfma_f32_16x16x32_bf16 v[6:9], v[206:209], v[198:201], v[6:9]
	v_mfma_f32_16x16x32_bf16 v[2:5], v[214:217], v[198:201], v[2:5]
	v_mfma_f32_16x16x32_bf16 v[54:57], v[210:213], v[178:181], v[54:57]
	v_mfma_f32_16x16x32_bf16 v[50:53], v[218:221], v[178:181], v[50:53]
	v_mfma_f32_16x16x32_bf16 v[38:41], v[210:213], v[186:189], v[38:41]
	v_mfma_f32_16x16x32_bf16 v[34:37], v[218:221], v[186:189], v[34:37]
	v_mfma_f32_16x16x32_bf16 v[22:25], v[210:213], v[194:197], v[22:25]
	v_mfma_f32_16x16x32_bf16 v[18:21], v[218:221], v[194:197], v[18:21]
	v_mfma_f32_16x16x32_bf16 v[6:9], v[210:213], v[202:205], v[6:9]
	v_mfma_f32_16x16x32_bf16 v[2:5], v[218:221], v[202:205], v[2:5]
	s_setprio 0
	s_add_i32 s56, s56, 2
	s_add_u32 s24, s24, 0x100
	s_addc_u32 s25, s25, 0
	s_add_u32 s54, s54, 0x100
	s_addc_u32 s55, s55, 0
	s_cmp_gt_u32 s56, 13
	s_barrier
	s_cbranch_scc0 .LBB0_3243
	v_lshl_or_b32 v142, s51, 8, v157
	v_lshl_add_u32 v144, s22, 8, v155
	v_ashrrev_i32_e32 v143, 31, v142
	v_mov_b64_e32 v[146:147], s[6:7]
	v_ashrrev_i32_e32 v145, 31, v144
	v_mad_i64_i32 v[162:163], s[24:25], v144, s49, v[146:147]
	v_lshlrev_b64 v[142:143], 1, v[142:143]
	v_lshl_add_u64 v[162:163], v[162:163], 0, v[142:143]
	v_lshlrev_b64 v[166:167], 12, v[144:145]
	v_add_co_u32_e32 v164, vcc, 0x2ec41000, v162
	v_lshl_add_u64 v[166:167], s[10:11], 0, v[166:167]
	s_nop 0
	v_addc_co_u32_e32 v165, vcc, 0, v163, vcc
	v_lshl_add_u64 v[166:167], v[166:167], 0, v[142:143]
	v_mov_b32_e32 v228, v164
	v_mov_b32_e32 v229, v165
	v_mov_b32_e32 v232, v166
	v_mov_b32_e32 v233, v167
	v_mov_b32_e32 v237, 0x1000
	global_load_dwordx2 v[174:175], v[228:229], off
	global_load_dwordx2 v[176:177], v[232:233], off
	global_load_dwordx2 v[178:179], v[228:229], off offset:32
	global_load_dwordx2 v[180:181], v[232:233], off offset:32
	global_load_dwordx2 v[182:183], v[228:229], off offset:256
	global_load_dwordx2 v[184:185], v[232:233], off offset:256
	global_load_dwordx2 v[186:187], v[228:229], off offset:288
	global_load_dwordx2 v[188:189], v[232:233], off offset:288
	v_mov_b32_e32 v236, 16
	v_mad_i64_i32 v[230:231], s[24:25], v236, s49, v[228:229]
	v_mad_i64_i32 v[234:235], s[24:25], v236, v237, v[232:233]
	global_load_dwordx2 v[190:191], v[230:231], off
	global_load_dwordx2 v[192:193], v[234:235], off
	global_load_dwordx2 v[194:195], v[230:231], off offset:32
	global_load_dwordx2 v[196:197], v[234:235], off offset:32
	global_load_dwordx2 v[198:199], v[230:231], off offset:256
	global_load_dwordx2 v[200:201], v[234:235], off offset:256
	global_load_dwordx2 v[202:203], v[230:231], off offset:288
	global_load_dwordx2 v[204:205], v[234:235], off offset:288
	v_mov_b32_e32 v236, 32
	v_mad_i64_i32 v[230:231], s[24:25], v236, s49, v[228:229]
	v_mad_i64_i32 v[234:235], s[24:25], v236, v237, v[232:233]
	global_load_dwordx2 v[206:207], v[230:231], off
	global_load_dwordx2 v[208:209], v[234:235], off
	global_load_dwordx2 v[210:211], v[230:231], off offset:32
	global_load_dwordx2 v[212:213], v[234:235], off offset:32
	global_load_dwordx2 v[214:215], v[230:231], off offset:256
	global_load_dwordx2 v[216:217], v[234:235], off offset:256
	global_load_dwordx2 v[218:219], v[230:231], off offset:288
	global_load_dwordx2 v[220:221], v[234:235], off offset:288
	s_waitcnt vmcnt(0)
	v_mov_b32_e32 v164, v174
	v_mov_b32_e32 v165, v175
	v_lshl_add_u64 v[162:163], v[162:163], 0, s[12:13]
	v_mov_b32_e32 v168, v176
	v_mov_b32_e32 v169, v177
	s_mov_b32 s51, s14
	s_mov_b32 s22, s16
	s_mov_b64 s[26:27], s[20:21]
	s_nop 0
	v_lshlrev_b32_e32 v170, 16, v164
	v_and_b32_e32 v171, 0xffff0000, v164
	v_lshlrev_b32_e32 v164, 16, v165
	v_and_b32_e32 v165, 0xffff0000, v165
	v_lshlrev_b32_e32 v172, 16, v168
	v_and_b32_e32 v173, 0xffff0000, v168
	v_lshlrev_b32_e32 v168, 16, v169
	v_and_b32_e32 v169, 0xffff0000, v169
	v_pk_fma_f32 v[128:129], v[128:129], v[164:165], v[168:169]
	v_pk_fma_f32 v[126:127], v[126:127], v[170:171], v[172:173]
	s_nop 0
	v_cvt_pk_bf16_f32 v126, v126, v127
	v_cvt_pk_bf16_f32 v127, v128, v129
	v_mov_b32_e32 v128, v178
	v_mov_b32_e32 v129, v179
	v_mov_b32_e32 v164, v180
	v_mov_b32_e32 v165, v181
	s_nop 0
	v_lshlrev_b32_e32 v168, 16, v164
	global_store_dwordx2 v[166:167], v[126:127], off
	v_lshlrev_b32_e32 v126, 16, v128
	v_and_b32_e32 v127, 0xffff0000, v128
	v_lshlrev_b32_e32 v128, 16, v129
	v_and_b32_e32 v129, 0xffff0000, v129
	v_and_b32_e32 v169, 0xffff0000, v164
	v_lshlrev_b32_e32 v164, 16, v165
	v_and_b32_e32 v165, 0xffff0000, v165
	v_pk_fma_f32 v[124:125], v[124:125], v[128:129], v[164:165]
	v_pk_fma_f32 v[122:123], v[122:123], v[126:127], v[168:169]
	s_nop 0
	v_cvt_pk_bf16_f32 v122, v122, v123
	v_cvt_pk_bf16_f32 v123, v124, v125
	v_mov_b32_e32 v124, v182
	v_mov_b32_e32 v125, v183
	v_mov_b32_e32 v126, v184
	v_mov_b32_e32 v127, v185
	s_nop 0
	v_lshlrev_b32_e32 v128, 16, v126
	global_store_dwordx2 v[166:167], v[122:123], off offset:32
	v_lshlrev_b32_e32 v122, 16, v124
	v_and_b32_e32 v123, 0xffff0000, v124
	v_lshlrev_b32_e32 v124, 16, v125
	v_and_b32_e32 v125, 0xffff0000, v125
	v_and_b32_e32 v129, 0xffff0000, v126
	v_lshlrev_b32_e32 v126, 16, v127
	v_and_b32_e32 v127, 0xffff0000, v127
	v_pk_fma_f32 v[120:121], v[120:121], v[124:125], v[126:127]
	v_pk_fma_f32 v[118:119], v[118:119], v[122:123], v[128:129]
	v_or_b32_e32 v124, 16, v144
	v_cvt_pk_bf16_f32 v118, v118, v119
	v_cvt_pk_bf16_f32 v119, v120, v121
	v_mov_b32_e32 v120, v186
	v_mov_b32_e32 v121, v187
	v_mov_b32_e32 v122, v188
	v_mov_b32_e32 v123, v189
	v_ashrrev_i32_e32 v125, 31, v124
	v_mad_i64_i32 v[126:127], s[24:25], v124, s49, v[146:147]
	global_store_dwordx2 v[166:167], v[118:119], off offset:256
	v_lshl_add_u64 v[126:127], v[126:127], 0, v[142:143]
	v_add_co_u32_e32 v128, vcc, s50, v126
	s_nop 0
	v_lshlrev_b32_e32 v118, 16, v120
	v_and_b32_e32 v119, 0xffff0000, v120
	v_lshlrev_b32_e32 v162, 16, v122
	v_and_b32_e32 v163, 0xffff0000, v122
	v_pk_fma_f32 v[114:115], v[114:115], v[118:119], v[162:163]
	v_lshlrev_b64 v[118:119], 12, v[124:125]
	v_lshlrev_b32_e32 v120, 16, v121
	v_and_b32_e32 v121, 0xffff0000, v121
	v_lshlrev_b32_e32 v122, 16, v123
	v_and_b32_e32 v123, 0xffff0000, v123
	v_lshl_add_u64 v[118:119], s[10:11], 0, v[118:119]
	v_addc_co_u32_e32 v129, vcc, 0, v127, vcc
	v_pk_fma_f32 v[116:117], v[116:117], v[120:121], v[122:123]
	v_lshl_add_u64 v[118:119], v[118:119], 0, v[142:143]
	v_cvt_pk_bf16_f32 v114, v114, v115
	v_cvt_pk_bf16_f32 v115, v116, v117
	v_mov_b32_e32 v116, v190
	v_mov_b32_e32 v117, v191
	v_mov_b32_e32 v120, v192
	v_mov_b32_e32 v121, v193
	v_lshl_add_u64 v[122:123], v[126:127], 0, s[12:13]
	global_store_dwordx2 v[166:167], v[114:115], off offset:288
	s_nop 0
	v_lshlrev_b32_e32 v114, 16, v116
	v_and_b32_e32 v115, 0xffff0000, v116
	v_lshlrev_b32_e32 v116, 16, v117
	v_and_b32_e32 v117, 0xffff0000, v117
	v_lshlrev_b32_e32 v124, 16, v120
	v_and_b32_e32 v125, 0xffff0000, v120
	v_lshlrev_b32_e32 v120, 16, v121
	v_and_b32_e32 v121, 0xffff0000, v121
	v_pk_fma_f32 v[112:113], v[112:113], v[116:117], v[120:121]
	v_pk_fma_f32 v[110:111], v[110:111], v[114:115], v[124:125]
	s_nop 0
	v_cvt_pk_bf16_f32 v110, v110, v111
	v_cvt_pk_bf16_f32 v111, v112, v113
	v_mov_b32_e32 v112, v194
	v_mov_b32_e32 v113, v195
	v_mov_b32_e32 v114, v196
	v_mov_b32_e32 v115, v197
	s_nop 0
	v_lshlrev_b32_e32 v116, 16, v114
	global_store_dwordx2 v[118:119], v[110:111], off
	v_lshlrev_b32_e32 v110, 16, v112
	v_and_b32_e32 v111, 0xffff0000, v112
	v_lshlrev_b32_e32 v112, 16, v113
	v_and_b32_e32 v113, 0xffff0000, v113
	v_and_b32_e32 v117, 0xffff0000, v114
	v_lshlrev_b32_e32 v114, 16, v115
	v_and_b32_e32 v115, 0xffff0000, v115
	v_pk_fma_f32 v[108:109], v[108:109], v[112:113], v[114:115]
	v_pk_fma_f32 v[106:107], v[106:107], v[110:111], v[116:117]
	s_nop 0
	v_cvt_pk_bf16_f32 v106, v106, v107
	v_cvt_pk_bf16_f32 v107, v108, v109
	v_mov_b32_e32 v108, v198
	v_mov_b32_e32 v109, v199
	v_mov_b32_e32 v110, v200
	v_mov_b32_e32 v111, v201
	s_nop 0
	v_lshlrev_b32_e32 v112, 16, v110
	global_store_dwordx2 v[118:119], v[106:107], off offset:32
	v_lshlrev_b32_e32 v106, 16, v108
	v_and_b32_e32 v107, 0xffff0000, v108
	v_lshlrev_b32_e32 v108, 16, v109
	v_and_b32_e32 v109, 0xffff0000, v109
	v_and_b32_e32 v113, 0xffff0000, v110
	v_lshlrev_b32_e32 v110, 16, v111
	v_and_b32_e32 v111, 0xffff0000, v111
	v_pk_fma_f32 v[104:105], v[104:105], v[108:109], v[110:111]
	v_pk_fma_f32 v[102:103], v[102:103], v[106:107], v[112:113]
	v_or_b32_e32 v108, 32, v144
	v_cvt_pk_bf16_f32 v102, v102, v103
	v_cvt_pk_bf16_f32 v103, v104, v105
	v_mov_b32_e32 v104, v202
	v_mov_b32_e32 v105, v203
	v_mov_b32_e32 v106, v204
	v_mov_b32_e32 v107, v205
	v_ashrrev_i32_e32 v109, 31, v108
	v_mad_i64_i32 v[110:111], s[24:25], v108, s49, v[146:147]
	global_store_dwordx2 v[118:119], v[102:103], off offset:256
	v_lshl_add_u64 v[110:111], v[110:111], 0, v[142:143]
	v_add_co_u32_e32 v112, vcc, s50, v110
	s_nop 0
	v_lshlrev_b32_e32 v102, 16, v104
	v_and_b32_e32 v103, 0xffff0000, v104
	v_lshlrev_b32_e32 v114, 16, v106
	v_and_b32_e32 v115, 0xffff0000, v106
	v_pk_fma_f32 v[98:99], v[98:99], v[102:103], v[114:115]
	v_lshlrev_b64 v[102:103], 12, v[108:109]
	v_lshlrev_b32_e32 v104, 16, v105
	v_and_b32_e32 v105, 0xffff0000, v105
	v_lshlrev_b32_e32 v106, 16, v107
	v_and_b32_e32 v107, 0xffff0000, v107
	v_lshl_add_u64 v[102:103], s[10:11], 0, v[102:103]
	v_addc_co_u32_e32 v113, vcc, 0, v111, vcc
	v_pk_fma_f32 v[100:101], v[100:101], v[104:105], v[106:107]
	v_lshl_add_u64 v[102:103], v[102:103], 0, v[142:143]
	v_cvt_pk_bf16_f32 v98, v98, v99
	v_cvt_pk_bf16_f32 v99, v100, v101
	v_mov_b32_e32 v100, v206
	v_mov_b32_e32 v101, v207
	v_mov_b32_e32 v104, v208
	v_mov_b32_e32 v105, v209
	v_lshl_add_u64 v[106:107], v[110:111], 0, s[12:13]
	global_store_dwordx2 v[118:119], v[98:99], off offset:288
	s_nop 0
	v_lshlrev_b32_e32 v98, 16, v100
	v_and_b32_e32 v99, 0xffff0000, v100
	v_lshlrev_b32_e32 v100, 16, v101
	v_and_b32_e32 v101, 0xffff0000, v101
	v_lshlrev_b32_e32 v108, 16, v104
	v_and_b32_e32 v109, 0xffff0000, v104
	v_lshlrev_b32_e32 v104, 16, v105
	v_and_b32_e32 v105, 0xffff0000, v105
	v_pk_fma_f32 v[96:97], v[96:97], v[100:101], v[104:105]
	v_pk_fma_f32 v[94:95], v[94:95], v[98:99], v[108:109]
	s_nop 0
	v_cvt_pk_bf16_f32 v94, v94, v95
	v_cvt_pk_bf16_f32 v95, v96, v97
	v_mov_b32_e32 v96, v210
	v_mov_b32_e32 v97, v211
	v_mov_b32_e32 v98, v212
	v_mov_b32_e32 v99, v213
	s_nop 0
	v_lshlrev_b32_e32 v100, 16, v98
	global_store_dwordx2 v[102:103], v[94:95], off
	v_lshlrev_b32_e32 v94, 16, v96
	v_and_b32_e32 v95, 0xffff0000, v96
	v_lshlrev_b32_e32 v96, 16, v97
	v_and_b32_e32 v97, 0xffff0000, v97
	v_and_b32_e32 v101, 0xffff0000, v98
	v_lshlrev_b32_e32 v98, 16, v99
	v_and_b32_e32 v99, 0xffff0000, v99
	v_pk_fma_f32 v[92:93], v[92:93], v[96:97], v[98:99]
	v_pk_fma_f32 v[90:91], v[90:91], v[94:95], v[100:101]
	s_nop 0
	v_cvt_pk_bf16_f32 v90, v90, v91
	v_cvt_pk_bf16_f32 v91, v92, v93
	v_mov_b32_e32 v92, v214
	v_mov_b32_e32 v93, v215
	v_mov_b32_e32 v94, v216
	v_mov_b32_e32 v95, v217
	s_nop 0
	v_lshlrev_b32_e32 v96, 16, v94
	global_store_dwordx2 v[102:103], v[90:91], off offset:32
	v_lshlrev_b32_e32 v90, 16, v92
	v_and_b32_e32 v91, 0xffff0000, v92
	v_lshlrev_b32_e32 v92, 16, v93
	v_and_b32_e32 v93, 0xffff0000, v93
	v_and_b32_e32 v97, 0xffff0000, v94
	v_lshlrev_b32_e32 v94, 16, v95
	v_and_b32_e32 v95, 0xffff0000, v95
	v_pk_fma_f32 v[88:89], v[88:89], v[92:93], v[94:95]
	v_pk_fma_f32 v[86:87], v[86:87], v[90:91], v[96:97]
	v_or_b32_e32 v92, 48, v144
	v_cvt_pk_bf16_f32 v86, v86, v87
	v_cvt_pk_bf16_f32 v87, v88, v89
	v_mov_b32_e32 v88, v218
	v_mov_b32_e32 v89, v219
	v_mov_b32_e32 v90, v220
	v_mov_b32_e32 v91, v221
	v_ashrrev_i32_e32 v93, 31, v92
	v_mad_i64_i32 v[94:95], s[24:25], v92, s49, v[146:147]
	global_store_dwordx2 v[102:103], v[86:87], off offset:256
	v_lshl_add_u64 v[94:95], v[94:95], 0, v[142:143]
	v_add_co_u32_e32 v96, vcc, s50, v94
	s_nop 0
	v_lshlrev_b32_e32 v86, 16, v88
	v_and_b32_e32 v87, 0xffff0000, v88
	v_lshlrev_b32_e32 v98, 16, v90
	v_and_b32_e32 v99, 0xffff0000, v90
	v_pk_fma_f32 v[82:83], v[82:83], v[86:87], v[98:99]
	v_lshlrev_b64 v[86:87], 12, v[92:93]
	v_lshlrev_b32_e32 v88, 16, v89
	v_and_b32_e32 v89, 0xffff0000, v89
	v_lshlrev_b32_e32 v90, 16, v91
	v_and_b32_e32 v91, 0xffff0000, v91
	v_lshl_add_u64 v[86:87], s[10:11], 0, v[86:87]
	v_addc_co_u32_e32 v97, vcc, 0, v95, vcc
	v_pk_fma_f32 v[84:85], v[84:85], v[88:89], v[90:91]
	v_lshl_add_u64 v[86:87], v[86:87], 0, v[142:143]
	v_cvt_pk_bf16_f32 v82, v82, v83
	v_cvt_pk_bf16_f32 v83, v84, v85
	v_mov_b32_e32 v237, 0x1000
	v_mov_b32_e32 v236, 48
	v_mad_i64_i32 v[230:231], s[24:25], v236, s49, v[228:229]
	v_mad_i64_i32 v[234:235], s[24:25], v236, v237, v[232:233]
	global_load_dwordx2 v[174:175], v[230:231], off
	global_load_dwordx2 v[176:177], v[234:235], off
	global_load_dwordx2 v[178:179], v[230:231], off offset:32
	global_load_dwordx2 v[180:181], v[234:235], off offset:32
	global_load_dwordx2 v[182:183], v[230:231], off offset:256
	global_load_dwordx2 v[184:185], v[234:235], off offset:256
	global_load_dwordx2 v[186:187], v[230:231], off offset:288
	global_load_dwordx2 v[188:189], v[234:235], off offset:288
	v_mov_b32_e32 v236, 128
	v_mad_i64_i32 v[230:231], s[24:25], v236, s49, v[228:229]
	v_mad_i64_i32 v[234:235], s[24:25], v236, v237, v[232:233]
	global_load_dwordx2 v[190:191], v[230:231], off
	global_load_dwordx2 v[192:193], v[234:235], off
	global_load_dwordx2 v[194:195], v[230:231], off offset:32
	global_load_dwordx2 v[196:197], v[234:235], off offset:32
	global_load_dwordx2 v[198:199], v[230:231], off offset:256
	global_load_dwordx2 v[200:201], v[234:235], off offset:256
	global_load_dwordx2 v[202:203], v[230:231], off offset:288
	global_load_dwordx2 v[204:205], v[234:235], off offset:288
	v_mov_b32_e32 v236, 144
	v_mad_i64_i32 v[230:231], s[24:25], v236, s49, v[228:229]
	v_mad_i64_i32 v[234:235], s[24:25], v236, v237, v[232:233]
	global_load_dwordx2 v[206:207], v[230:231], off
	global_load_dwordx2 v[208:209], v[234:235], off
	global_load_dwordx2 v[210:211], v[230:231], off offset:32
	global_load_dwordx2 v[212:213], v[234:235], off offset:32
	global_load_dwordx2 v[214:215], v[230:231], off offset:256
	global_load_dwordx2 v[216:217], v[234:235], off offset:256
	global_load_dwordx2 v[218:219], v[230:231], off offset:288
	global_load_dwordx2 v[220:221], v[234:235], off offset:288
	s_waitcnt vmcnt(0)
	v_mov_b32_e32 v84, v174
	v_mov_b32_e32 v85, v175
	v_mov_b32_e32 v88, v176
	v_mov_b32_e32 v89, v177
	v_lshl_add_u64 v[90:91], v[94:95], 0, s[12:13]
	global_store_dwordx2 v[102:103], v[82:83], off offset:288
	s_nop 0
	v_lshlrev_b32_e32 v82, 16, v84
	v_and_b32_e32 v83, 0xffff0000, v84
	v_lshlrev_b32_e32 v84, 16, v85
	v_and_b32_e32 v85, 0xffff0000, v85
	v_lshlrev_b32_e32 v92, 16, v88
	v_and_b32_e32 v93, 0xffff0000, v88
	v_lshlrev_b32_e32 v88, 16, v89
	v_and_b32_e32 v89, 0xffff0000, v89
	v_pk_fma_f32 v[80:81], v[80:81], v[84:85], v[88:89]
	v_pk_fma_f32 v[78:79], v[78:79], v[82:83], v[92:93]
	s_nop 0
	v_cvt_pk_bf16_f32 v78, v78, v79
	v_cvt_pk_bf16_f32 v79, v80, v81
	v_mov_b32_e32 v80, v178
	v_mov_b32_e32 v81, v179
	v_mov_b32_e32 v82, v180
	v_mov_b32_e32 v83, v181
	s_nop 0
	v_lshlrev_b32_e32 v84, 16, v82
	global_store_dwordx2 v[86:87], v[78:79], off
	v_lshlrev_b32_e32 v78, 16, v80
	v_and_b32_e32 v79, 0xffff0000, v80
	v_lshlrev_b32_e32 v80, 16, v81
	v_and_b32_e32 v81, 0xffff0000, v81
	v_and_b32_e32 v85, 0xffff0000, v82
	v_lshlrev_b32_e32 v82, 16, v83
	v_and_b32_e32 v83, 0xffff0000, v83
	v_pk_fma_f32 v[76:77], v[76:77], v[80:81], v[82:83]
	v_pk_fma_f32 v[74:75], v[74:75], v[78:79], v[84:85]
	s_nop 0
	v_cvt_pk_bf16_f32 v74, v74, v75
	v_cvt_pk_bf16_f32 v75, v76, v77
	v_mov_b32_e32 v76, v182
	v_mov_b32_e32 v77, v183
	v_mov_b32_e32 v78, v184
	v_mov_b32_e32 v79, v185
	s_nop 0
	v_lshlrev_b32_e32 v80, 16, v78
	global_store_dwordx2 v[86:87], v[74:75], off offset:32
	v_lshlrev_b32_e32 v74, 16, v76
	v_and_b32_e32 v75, 0xffff0000, v76
	v_lshlrev_b32_e32 v76, 16, v77
	v_and_b32_e32 v77, 0xffff0000, v77
	v_and_b32_e32 v81, 0xffff0000, v78
	v_lshlrev_b32_e32 v78, 16, v79
	v_and_b32_e32 v79, 0xffff0000, v79
	v_pk_fma_f32 v[72:73], v[72:73], v[76:77], v[78:79]
	v_pk_fma_f32 v[70:71], v[70:71], v[74:75], v[80:81]
	v_add_u32_e32 v76, 0x80, v144
	v_cvt_pk_bf16_f32 v70, v70, v71
	v_cvt_pk_bf16_f32 v71, v72, v73
	v_mov_b32_e32 v72, v186
	v_mov_b32_e32 v73, v187
	v_mov_b32_e32 v74, v188
	v_mov_b32_e32 v75, v189
	v_ashrrev_i32_e32 v77, 31, v76
	v_mad_i64_i32 v[78:79], s[24:25], v76, s49, v[146:147]
	global_store_dwordx2 v[86:87], v[70:71], off offset:256
	v_lshl_add_u64 v[78:79], v[78:79], 0, v[142:143]
	v_add_co_u32_e32 v80, vcc, s50, v78
	s_nop 0
	v_lshlrev_b32_e32 v70, 16, v72
	v_and_b32_e32 v71, 0xffff0000, v72
	v_lshlrev_b32_e32 v82, 16, v74
	v_and_b32_e32 v83, 0xffff0000, v74
	v_pk_fma_f32 v[66:67], v[66:67], v[70:71], v[82:83]
	v_lshlrev_b64 v[70:71], 12, v[76:77]
	v_lshlrev_b32_e32 v72, 16, v73
	v_and_b32_e32 v73, 0xffff0000, v73
	v_lshlrev_b32_e32 v74, 16, v75
	v_and_b32_e32 v75, 0xffff0000, v75
	v_lshl_add_u64 v[70:71], s[10:11], 0, v[70:71]
	v_addc_co_u32_e32 v81, vcc, 0, v79, vcc
	v_pk_fma_f32 v[68:69], v[68:69], v[72:73], v[74:75]
	v_lshl_add_u64 v[70:71], v[70:71], 0, v[142:143]
	v_cvt_pk_bf16_f32 v66, v66, v67
	v_cvt_pk_bf16_f32 v67, v68, v69
	v_mov_b32_e32 v68, v190
	v_mov_b32_e32 v69, v191
	v_mov_b32_e32 v72, v192
	v_mov_b32_e32 v73, v193
	v_lshl_add_u64 v[74:75], v[78:79], 0, s[12:13]
	global_store_dwordx2 v[86:87], v[66:67], off offset:288
	s_nop 0
	v_lshlrev_b32_e32 v66, 16, v68
	v_and_b32_e32 v67, 0xffff0000, v68
	v_lshlrev_b32_e32 v68, 16, v69
	v_and_b32_e32 v69, 0xffff0000, v69
	v_lshlrev_b32_e32 v76, 16, v72
	v_and_b32_e32 v77, 0xffff0000, v72
	v_lshlrev_b32_e32 v72, 16, v73
	v_and_b32_e32 v73, 0xffff0000, v73
	v_pk_fma_f32 v[64:65], v[64:65], v[68:69], v[72:73]
	v_pk_fma_f32 v[62:63], v[62:63], v[66:67], v[76:77]
	s_nop 0
	v_cvt_pk_bf16_f32 v62, v62, v63
	v_cvt_pk_bf16_f32 v63, v64, v65
	v_mov_b32_e32 v64, v194
	v_mov_b32_e32 v65, v195
	v_mov_b32_e32 v66, v196
	v_mov_b32_e32 v67, v197
	s_nop 0
	v_lshlrev_b32_e32 v68, 16, v66
	global_store_dwordx2 v[70:71], v[62:63], off
	v_lshlrev_b32_e32 v62, 16, v64
	v_and_b32_e32 v63, 0xffff0000, v64
	v_lshlrev_b32_e32 v64, 16, v65
	v_and_b32_e32 v65, 0xffff0000, v65
	v_and_b32_e32 v69, 0xffff0000, v66
	v_lshlrev_b32_e32 v66, 16, v67
	v_and_b32_e32 v67, 0xffff0000, v67
	v_pk_fma_f32 v[60:61], v[60:61], v[64:65], v[66:67]
	v_pk_fma_f32 v[58:59], v[58:59], v[62:63], v[68:69]
	s_nop 0
	v_cvt_pk_bf16_f32 v58, v58, v59
	v_cvt_pk_bf16_f32 v59, v60, v61
	v_mov_b32_e32 v60, v198
	v_mov_b32_e32 v61, v199
	v_mov_b32_e32 v62, v200
	v_mov_b32_e32 v63, v201
	s_nop 0
	v_lshlrev_b32_e32 v64, 16, v62
	global_store_dwordx2 v[70:71], v[58:59], off offset:32
	v_lshlrev_b32_e32 v58, 16, v60
	v_and_b32_e32 v59, 0xffff0000, v60
	v_lshlrev_b32_e32 v60, 16, v61
	v_and_b32_e32 v61, 0xffff0000, v61
	v_and_b32_e32 v65, 0xffff0000, v62
	v_lshlrev_b32_e32 v62, 16, v63
	v_and_b32_e32 v63, 0xffff0000, v63
	v_pk_fma_f32 v[56:57], v[56:57], v[60:61], v[62:63]
	v_pk_fma_f32 v[54:55], v[54:55], v[58:59], v[64:65]
	v_add_u32_e32 v60, 0x90, v144
	v_cvt_pk_bf16_f32 v54, v54, v55
	v_cvt_pk_bf16_f32 v55, v56, v57
	v_mov_b32_e32 v56, v202
	v_mov_b32_e32 v57, v203
	v_mov_b32_e32 v58, v204
	v_mov_b32_e32 v59, v205
	v_ashrrev_i32_e32 v61, 31, v60
	v_mad_i64_i32 v[62:63], s[24:25], v60, s49, v[146:147]
	global_store_dwordx2 v[70:71], v[54:55], off offset:256
	v_lshl_add_u64 v[62:63], v[62:63], 0, v[142:143]
	v_add_co_u32_e32 v64, vcc, s50, v62
	s_nop 0
	v_lshlrev_b32_e32 v54, 16, v56
	v_and_b32_e32 v55, 0xffff0000, v56
	v_lshlrev_b32_e32 v66, 16, v58
	v_and_b32_e32 v67, 0xffff0000, v58
	v_pk_fma_f32 v[50:51], v[50:51], v[54:55], v[66:67]
	v_lshlrev_b64 v[54:55], 12, v[60:61]
	v_lshlrev_b32_e32 v56, 16, v57
	v_and_b32_e32 v57, 0xffff0000, v57
	v_lshlrev_b32_e32 v58, 16, v59
	v_and_b32_e32 v59, 0xffff0000, v59
	v_lshl_add_u64 v[54:55], s[10:11], 0, v[54:55]
	v_addc_co_u32_e32 v65, vcc, 0, v63, vcc
	v_pk_fma_f32 v[52:53], v[52:53], v[56:57], v[58:59]
	v_lshl_add_u64 v[54:55], v[54:55], 0, v[142:143]
	v_cvt_pk_bf16_f32 v50, v50, v51
	v_cvt_pk_bf16_f32 v51, v52, v53
	v_mov_b32_e32 v52, v206
	v_mov_b32_e32 v53, v207
	v_mov_b32_e32 v56, v208
	v_mov_b32_e32 v57, v209
	v_lshl_add_u64 v[58:59], v[62:63], 0, s[12:13]
	global_store_dwordx2 v[70:71], v[50:51], off offset:288
	s_nop 0
	v_lshlrev_b32_e32 v50, 16, v52
	v_and_b32_e32 v51, 0xffff0000, v52
	v_lshlrev_b32_e32 v52, 16, v53
	v_and_b32_e32 v53, 0xffff0000, v53
	v_lshlrev_b32_e32 v60, 16, v56
	v_and_b32_e32 v61, 0xffff0000, v56
	v_lshlrev_b32_e32 v56, 16, v57
	v_and_b32_e32 v57, 0xffff0000, v57
	v_pk_fma_f32 v[48:49], v[48:49], v[52:53], v[56:57]
	v_pk_fma_f32 v[46:47], v[46:47], v[50:51], v[60:61]
	s_nop 0
	v_cvt_pk_bf16_f32 v46, v46, v47
	v_cvt_pk_bf16_f32 v47, v48, v49
	v_mov_b32_e32 v48, v210
	v_mov_b32_e32 v49, v211
	v_mov_b32_e32 v50, v212
	v_mov_b32_e32 v51, v213
	s_nop 0
	v_lshlrev_b32_e32 v52, 16, v50
	global_store_dwordx2 v[54:55], v[46:47], off
	v_lshlrev_b32_e32 v46, 16, v48
	v_and_b32_e32 v47, 0xffff0000, v48
	v_lshlrev_b32_e32 v48, 16, v49
	v_and_b32_e32 v49, 0xffff0000, v49
	v_and_b32_e32 v53, 0xffff0000, v50
	v_lshlrev_b32_e32 v50, 16, v51
	v_and_b32_e32 v51, 0xffff0000, v51
	v_pk_fma_f32 v[44:45], v[44:45], v[48:49], v[50:51]
	v_pk_fma_f32 v[42:43], v[42:43], v[46:47], v[52:53]
	s_nop 0
	v_cvt_pk_bf16_f32 v42, v42, v43
	v_cvt_pk_bf16_f32 v43, v44, v45
	v_mov_b32_e32 v44, v214
	v_mov_b32_e32 v45, v215
	v_mov_b32_e32 v46, v216
	v_mov_b32_e32 v47, v217
	s_nop 0
	v_lshlrev_b32_e32 v48, 16, v46
	global_store_dwordx2 v[54:55], v[42:43], off offset:32
	v_lshlrev_b32_e32 v42, 16, v44
	v_and_b32_e32 v43, 0xffff0000, v44
	v_lshlrev_b32_e32 v44, 16, v45
	v_and_b32_e32 v45, 0xffff0000, v45
	v_and_b32_e32 v49, 0xffff0000, v46
	v_lshlrev_b32_e32 v46, 16, v47
	v_and_b32_e32 v47, 0xffff0000, v47
	v_pk_fma_f32 v[40:41], v[40:41], v[44:45], v[46:47]
	v_pk_fma_f32 v[38:39], v[38:39], v[42:43], v[48:49]
	v_add_u32_e32 v44, 0xa0, v144
	v_cvt_pk_bf16_f32 v38, v38, v39
	v_cvt_pk_bf16_f32 v39, v40, v41
	v_mov_b32_e32 v40, v218
	v_mov_b32_e32 v41, v219
	v_mov_b32_e32 v42, v220
	v_mov_b32_e32 v43, v221
	v_ashrrev_i32_e32 v45, 31, v44
	v_mad_i64_i32 v[46:47], s[24:25], v44, s49, v[146:147]
	global_store_dwordx2 v[54:55], v[38:39], off offset:256
	v_lshl_add_u64 v[46:47], v[46:47], 0, v[142:143]
	v_add_co_u32_e32 v48, vcc, s50, v46
	s_nop 0
	v_lshlrev_b32_e32 v38, 16, v40
	v_and_b32_e32 v39, 0xffff0000, v40
	v_lshlrev_b32_e32 v50, 16, v42
	v_and_b32_e32 v51, 0xffff0000, v42
	v_pk_fma_f32 v[34:35], v[34:35], v[38:39], v[50:51]
	v_lshlrev_b64 v[38:39], 12, v[44:45]
	v_lshlrev_b32_e32 v40, 16, v41
	v_and_b32_e32 v41, 0xffff0000, v41
	v_lshlrev_b32_e32 v42, 16, v43
	v_and_b32_e32 v43, 0xffff0000, v43
	v_lshl_add_u64 v[38:39], s[10:11], 0, v[38:39]
	v_addc_co_u32_e32 v49, vcc, 0, v47, vcc
	v_pk_fma_f32 v[36:37], v[36:37], v[40:41], v[42:43]
	v_lshl_add_u64 v[38:39], v[38:39], 0, v[142:143]
	v_cvt_pk_bf16_f32 v34, v34, v35
	v_cvt_pk_bf16_f32 v35, v36, v37
	v_mov_b32_e32 v237, 0x1000
	v_mov_b32_e32 v236, 160
	v_mad_i64_i32 v[230:231], s[24:25], v236, s49, v[228:229]
	v_mad_i64_i32 v[234:235], s[24:25], v236, v237, v[232:233]
	global_load_dwordx2 v[174:175], v[230:231], off
	global_load_dwordx2 v[176:177], v[234:235], off
	global_load_dwordx2 v[178:179], v[230:231], off offset:32
	global_load_dwordx2 v[180:181], v[234:235], off offset:32
	global_load_dwordx2 v[182:183], v[230:231], off offset:256
	global_load_dwordx2 v[184:185], v[234:235], off offset:256
	global_load_dwordx2 v[186:187], v[230:231], off offset:288
	global_load_dwordx2 v[188:189], v[234:235], off offset:288
	v_mov_b32_e32 v236, 176
	v_mad_i64_i32 v[230:231], s[24:25], v236, s49, v[228:229]
	v_mad_i64_i32 v[234:235], s[24:25], v236, v237, v[232:233]
	global_load_dwordx2 v[190:191], v[230:231], off
	global_load_dwordx2 v[192:193], v[234:235], off
	global_load_dwordx2 v[194:195], v[230:231], off offset:32
	global_load_dwordx2 v[196:197], v[234:235], off offset:32
	global_load_dwordx2 v[198:199], v[230:231], off offset:256
	global_load_dwordx2 v[200:201], v[234:235], off offset:256
	global_load_dwordx2 v[202:203], v[230:231], off offset:288
	global_load_dwordx2 v[204:205], v[234:235], off offset:288
	s_waitcnt vmcnt(0)
	v_mov_b32_e32 v36, v174
	v_mov_b32_e32 v37, v175
	v_mov_b32_e32 v40, v176
	v_mov_b32_e32 v41, v177
	v_lshl_add_u64 v[42:43], v[46:47], 0, s[12:13]
	global_store_dwordx2 v[54:55], v[34:35], off offset:288
	s_nop 0
	v_lshlrev_b32_e32 v34, 16, v36
	v_and_b32_e32 v35, 0xffff0000, v36
	v_lshlrev_b32_e32 v36, 16, v37
	v_and_b32_e32 v37, 0xffff0000, v37
	v_lshlrev_b32_e32 v44, 16, v40
	v_and_b32_e32 v45, 0xffff0000, v40
	v_lshlrev_b32_e32 v40, 16, v41
	v_and_b32_e32 v41, 0xffff0000, v41
	v_pk_fma_f32 v[32:33], v[32:33], v[36:37], v[40:41]
	v_pk_fma_f32 v[30:31], v[30:31], v[34:35], v[44:45]
	s_nop 0
	v_cvt_pk_bf16_f32 v30, v30, v31
	v_cvt_pk_bf16_f32 v31, v32, v33
	v_mov_b32_e32 v32, v178
	v_mov_b32_e32 v33, v179
	v_mov_b32_e32 v34, v180
	v_mov_b32_e32 v35, v181
	s_nop 0
	v_lshlrev_b32_e32 v36, 16, v34
	global_store_dwordx2 v[38:39], v[30:31], off
	v_lshlrev_b32_e32 v30, 16, v32
	v_and_b32_e32 v31, 0xffff0000, v32
	v_lshlrev_b32_e32 v32, 16, v33
	v_and_b32_e32 v33, 0xffff0000, v33
	v_and_b32_e32 v37, 0xffff0000, v34
	v_lshlrev_b32_e32 v34, 16, v35
	v_and_b32_e32 v35, 0xffff0000, v35
	v_pk_fma_f32 v[28:29], v[28:29], v[32:33], v[34:35]
	v_pk_fma_f32 v[26:27], v[26:27], v[30:31], v[36:37]
	s_nop 0
	v_cvt_pk_bf16_f32 v26, v26, v27
	v_cvt_pk_bf16_f32 v27, v28, v29
	v_mov_b32_e32 v28, v182
	v_mov_b32_e32 v29, v183
	v_mov_b32_e32 v30, v184
	v_mov_b32_e32 v31, v185
	s_nop 0
	v_lshlrev_b32_e32 v32, 16, v30
	global_store_dwordx2 v[38:39], v[26:27], off offset:32
	v_lshlrev_b32_e32 v26, 16, v28
	v_and_b32_e32 v27, 0xffff0000, v28
	v_lshlrev_b32_e32 v28, 16, v29
	v_and_b32_e32 v29, 0xffff0000, v29
	v_and_b32_e32 v33, 0xffff0000, v30
	v_lshlrev_b32_e32 v30, 16, v31
	v_and_b32_e32 v31, 0xffff0000, v31
	v_pk_fma_f32 v[24:25], v[24:25], v[28:29], v[30:31]
	v_pk_fma_f32 v[22:23], v[22:23], v[26:27], v[32:33]
	v_add_u32_e32 v28, 0xb0, v144
	v_cvt_pk_bf16_f32 v22, v22, v23
	v_cvt_pk_bf16_f32 v23, v24, v25
	v_mov_b32_e32 v24, v186
	v_mov_b32_e32 v25, v187
	v_mov_b32_e32 v26, v188
	v_mov_b32_e32 v27, v189
	v_ashrrev_i32_e32 v29, 31, v28
	v_mad_i64_i32 v[30:31], s[24:25], v28, s49, v[146:147]
	global_store_dwordx2 v[38:39], v[22:23], off offset:256
	v_lshl_add_u64 v[30:31], v[30:31], 0, v[142:143]
	v_add_co_u32_e32 v32, vcc, s50, v30
	s_mov_b64 s[24:25], s[18:19]
	s_nop 0
	v_addc_co_u32_e32 v33, vcc, 0, v31, vcc
	s_and_b64 vcc, exec, s[2:3]
	s_nop 0
	v_lshlrev_b32_e32 v22, 16, v24
	v_and_b32_e32 v23, 0xffff0000, v24
	v_lshlrev_b32_e32 v34, 16, v26
	v_and_b32_e32 v35, 0xffff0000, v26
	v_pk_fma_f32 v[18:19], v[18:19], v[22:23], v[34:35]
	v_lshlrev_b64 v[22:23], 12, v[28:29]
	v_lshlrev_b32_e32 v24, 16, v25
	v_and_b32_e32 v25, 0xffff0000, v25
	v_lshlrev_b32_e32 v26, 16, v27
	v_and_b32_e32 v27, 0xffff0000, v27
	v_lshl_add_u64 v[22:23], s[10:11], 0, v[22:23]
	v_pk_fma_f32 v[20:21], v[20:21], v[24:25], v[26:27]
	v_lshl_add_u64 v[22:23], v[22:23], 0, v[142:143]
	v_cvt_pk_bf16_f32 v18, v18, v19
	v_cvt_pk_bf16_f32 v19, v20, v21
	v_mov_b32_e32 v20, v190
	v_mov_b32_e32 v21, v191
	v_mov_b32_e32 v24, v192
	v_mov_b32_e32 v25, v193
	v_lshl_add_u64 v[26:27], v[30:31], 0, s[12:13]
	global_store_dwordx2 v[38:39], v[18:19], off offset:288
	s_nop 0
	v_lshlrev_b32_e32 v18, 16, v20
	v_and_b32_e32 v19, 0xffff0000, v20
	v_lshlrev_b32_e32 v20, 16, v21
	v_and_b32_e32 v21, 0xffff0000, v21
	v_lshlrev_b32_e32 v28, 16, v24
	v_and_b32_e32 v29, 0xffff0000, v24
	v_lshlrev_b32_e32 v24, 16, v25
	v_and_b32_e32 v25, 0xffff0000, v25
	v_pk_fma_f32 v[16:17], v[16:17], v[20:21], v[24:25]
	v_pk_fma_f32 v[14:15], v[14:15], v[18:19], v[28:29]
	s_nop 0
	v_cvt_pk_bf16_f32 v14, v14, v15
	v_cvt_pk_bf16_f32 v15, v16, v17
	v_mov_b32_e32 v16, v194
	v_mov_b32_e32 v17, v195
	v_mov_b32_e32 v18, v196
	v_mov_b32_e32 v19, v197
	s_nop 0
	v_lshlrev_b32_e32 v20, 16, v18
	global_store_dwordx2 v[22:23], v[14:15], off
	v_lshlrev_b32_e32 v14, 16, v16
	v_and_b32_e32 v15, 0xffff0000, v16
	v_lshlrev_b32_e32 v16, 16, v17
	v_and_b32_e32 v17, 0xffff0000, v17
	v_and_b32_e32 v21, 0xffff0000, v18
	v_lshlrev_b32_e32 v18, 16, v19
	v_and_b32_e32 v19, 0xffff0000, v19
	v_pk_fma_f32 v[12:13], v[12:13], v[16:17], v[18:19]
	v_pk_fma_f32 v[10:11], v[10:11], v[14:15], v[20:21]
	s_nop 0
	v_cvt_pk_bf16_f32 v10, v10, v11
	v_cvt_pk_bf16_f32 v11, v12, v13
	v_mov_b32_e32 v12, v198
	v_mov_b32_e32 v13, v199
	v_mov_b32_e32 v14, v200
	v_mov_b32_e32 v15, v201
	s_nop 0
	v_lshlrev_b32_e32 v16, 16, v14
	global_store_dwordx2 v[22:23], v[10:11], off offset:32
	v_lshlrev_b32_e32 v10, 16, v12
	v_and_b32_e32 v11, 0xffff0000, v12
	v_lshlrev_b32_e32 v12, 16, v13
	v_and_b32_e32 v13, 0xffff0000, v13
	v_and_b32_e32 v17, 0xffff0000, v14
	v_lshlrev_b32_e32 v14, 16, v15
	v_and_b32_e32 v15, 0xffff0000, v15
	v_pk_fma_f32 v[8:9], v[8:9], v[12:13], v[14:15]
	v_pk_fma_f32 v[6:7], v[6:7], v[10:11], v[16:17]
	s_nop 0
	v_cvt_pk_bf16_f32 v6, v6, v7
	v_cvt_pk_bf16_f32 v7, v8, v9
	v_mov_b32_e32 v8, v202
	v_mov_b32_e32 v9, v203
	v_mov_b32_e32 v10, v204
	v_mov_b32_e32 v11, v205
	s_nop 0
	v_lshlrev_b32_e32 v12, 16, v10
	global_store_dwordx2 v[22:23], v[6:7], off offset:256
	v_lshlrev_b32_e32 v6, 16, v8
	v_and_b32_e32 v7, 0xffff0000, v8
	v_and_b32_e32 v13, 0xffff0000, v10
	v_lshlrev_b32_e32 v8, 16, v9
	v_and_b32_e32 v9, 0xffff0000, v9
	v_lshlrev_b32_e32 v10, 16, v11
	v_and_b32_e32 v11, 0xffff0000, v11
	v_pk_fma_f32 v[2:3], v[2:3], v[6:7], v[12:13]
	v_pk_fma_f32 v[4:5], v[4:5], v[8:9], v[10:11]
	v_cvt_pk_bf16_f32 v2, v2, v3
	s_nop 0
	v_cvt_pk_bf16_f32 v3, v4, v5
	global_store_dwordx2 v[22:23], v[2:3], off offset:288
	s_cbranch_vccz .LBB0_3240
	s_waitcnt vmcnt(0)
	s_cmpk_gt_u32 s33, 0xff
	s_cbranch_scc1 .LBB0_3247
	s_barrier

.LBB0_3255:
	ds_read_b128 v[142:145], v1
	ds_read_b128 v[156:159], v1 offset:1024
	ds_read_b128 v[160:163], v1 offset:2048
	ds_read_b128 v[164:167], v1 offset:3072
	s_add_u32 s24, s22, 0xfffc0080
	s_addc_u32 s25, s23, -1
	s_cmp_eq_u32 s54, 12
	s_cselect_b32 s27, s15, s25
	s_cselect_b32 s26, s50, s24
	s_cselect_b32 s25, s13, s53
	s_cselect_b32 s24, s51, s52
	v_lshl_add_u64 v[146:147], s[22:23], 0, v[134:135]
	s_add_i32 m0, s21, 0xc000
	ds_read_b128 v[168:171], v148
	ds_read_b128 v[172:175], v148 offset:1024
	ds_read_b128 v[176:179], v148 offset:2048
	ds_read_b128 v[180:183], v148 offset:3072
	ds_read_b128 v[184:187], v148 offset:4096
	ds_read_b128 v[188:191], v148 offset:5120
	ds_read_b128 v[192:195], v148 offset:6144
	ds_read_b128 v[196:199], v148 offset:7168
	global_load_lds_dwordx4 v[146:147], off
	v_lshl_add_u64 v[146:147], s[22:23], 0, v[136:137]
	s_add_i32 m0, s21, 0xe000
	s_nop 0
	global_load_lds_dwordx4 v[146:147], off
	s_waitcnt lgkmcnt(8)
	s_barrier
	s_waitcnt lgkmcnt(0)
	s_setprio 1
	s_waitcnt lgkmcnt(0)
	v_mfma_f32_16x16x32_bf16 v[126:129], v[142:145], v[168:171], v[126:129]
	v_mfma_f32_16x16x32_bf16 v[122:125], v[160:163], v[168:171], v[122:125]
	v_mfma_f32_16x16x32_bf16 v[110:113], v[142:145], v[176:179], v[110:113]
	v_mfma_f32_16x16x32_bf16 v[106:109], v[160:163], v[176:179], v[106:109]
	v_mfma_f32_16x16x32_bf16 v[94:97], v[142:145], v[184:187], v[94:97]
	v_mfma_f32_16x16x32_bf16 v[90:93], v[160:163], v[184:187], v[90:93]
	v_mfma_f32_16x16x32_bf16 v[78:81], v[142:145], v[192:195], v[78:81]
	v_mfma_f32_16x16x32_bf16 v[74:77], v[160:163], v[192:195], v[74:77]
	v_mfma_f32_16x16x32_bf16 v[126:129], v[156:159], v[172:175], v[126:129]
	v_mfma_f32_16x16x32_bf16 v[122:125], v[164:167], v[172:175], v[122:125]
	v_mfma_f32_16x16x32_bf16 v[110:113], v[156:159], v[180:183], v[110:113]
	v_mfma_f32_16x16x32_bf16 v[106:109], v[164:167], v[180:183], v[106:109]
	v_mfma_f32_16x16x32_bf16 v[94:97], v[156:159], v[188:191], v[94:97]
	v_mfma_f32_16x16x32_bf16 v[90:93], v[164:167], v[188:191], v[90:93]
	v_mfma_f32_16x16x32_bf16 v[78:81], v[156:159], v[196:199], v[78:81]
	v_mfma_f32_16x16x32_bf16 v[74:77], v[164:167], v[196:199], v[74:77]
	s_setprio 0
	s_barrier
	s_add_i32 s55, s45, s36
	v_lshl_add_u64 v[146:147], s[24:25], 0, v[130:131]
	s_mov_b32 m0, s55
	ds_read_b128 v[200:203], v149
	ds_read_b128 v[204:207], v149 offset:1024
	ds_read_b128 v[208:211], v149 offset:2048
	ds_read_b128 v[212:215], v149 offset:3072
	global_load_lds_dwordx4 v[146:147], off
	v_lshl_add_u64 v[216:217], s[24:25], 0, v[132:133]
	s_add_i32 m0, s55, 0x2000
	s_nop 0
	global_load_lds_dwordx4 v[216:217], off
	s_barrier
	s_waitcnt lgkmcnt(0)
	s_setprio 1
	s_waitcnt lgkmcnt(0)
	v_mfma_f32_16x16x32_bf16 v[118:121], v[200:203], v[168:171], v[118:121]
	v_mfma_f32_16x16x32_bf16 v[114:117], v[208:211], v[168:171], v[114:117]
	v_mfma_f32_16x16x32_bf16 v[102:105], v[200:203], v[176:179], v[102:105]
	v_mfma_f32_16x16x32_bf16 v[98:101], v[208:211], v[176:179], v[98:101]
	v_mfma_f32_16x16x32_bf16 v[86:89], v[200:203], v[184:187], v[86:89]
	v_mfma_f32_16x16x32_bf16 v[82:85], v[208:211], v[184:187], v[82:85]
	v_mfma_f32_16x16x32_bf16 v[70:73], v[200:203], v[192:195], v[70:73]
	v_mfma_f32_16x16x32_bf16 v[66:69], v[208:211], v[192:195], v[66:69]
	v_mfma_f32_16x16x32_bf16 v[118:121], v[204:207], v[172:175], v[118:121]
	v_mfma_f32_16x16x32_bf16 v[114:117], v[212:215], v[172:175], v[114:117]
	v_mfma_f32_16x16x32_bf16 v[102:105], v[204:207], v[180:183], v[102:105]
	v_mfma_f32_16x16x32_bf16 v[98:101], v[212:215], v[180:183], v[98:101]
	v_mfma_f32_16x16x32_bf16 v[86:89], v[204:207], v[188:191], v[86:89]
	v_mfma_f32_16x16x32_bf16 v[82:85], v[212:215], v[188:191], v[82:85]
	v_mfma_f32_16x16x32_bf16 v[70:73], v[204:207], v[196:199], v[70:73]
	v_mfma_f32_16x16x32_bf16 v[66:69], v[212:215], v[196:199], v[66:69]
	s_setprio 0
	s_mov_b32 m0, s21
	v_lshl_add_u64 v[218:219], s[26:27], 0, v[130:131]
	s_barrier
	ds_read_b128 v[168:171], v148 offset:16384
	ds_read_b128 v[172:175], v148 offset:17408
	ds_read_b128 v[176:179], v148 offset:18432
	ds_read_b128 v[180:183], v148 offset:19456
	ds_read_b128 v[184:187], v148 offset:20480
	ds_read_b128 v[188:191], v148 offset:21504
	ds_read_b128 v[192:195], v148 offset:22528
	ds_read_b128 v[196:199], v148 offset:23552
	global_load_lds_dwordx4 v[218:219], off
	v_lshl_add_u64 v[220:221], s[26:27], 0, v[132:133]
	s_mov_b32 m0, s38
	s_nop 0
	global_load_lds_dwordx4 v[220:221], off
	s_barrier
	s_waitcnt lgkmcnt(0)
	s_setprio 1
	s_waitcnt lgkmcnt(0)
	v_mfma_f32_16x16x32_bf16 v[62:65], v[142:145], v[168:171], v[62:65]
	v_mfma_f32_16x16x32_bf16 v[58:61], v[160:163], v[168:171], v[58:61]
	v_mfma_f32_16x16x32_bf16 v[46:49], v[142:145], v[176:179], v[46:49]
	v_mfma_f32_16x16x32_bf16 v[42:45], v[160:163], v[176:179], v[42:45]
	v_mfma_f32_16x16x32_bf16 v[30:33], v[142:145], v[184:187], v[30:33]
	v_mfma_f32_16x16x32_bf16 v[26:29], v[160:163], v[184:187], v[26:29]
	v_mfma_f32_16x16x32_bf16 v[14:17], v[142:145], v[192:195], v[14:17]
	v_mfma_f32_16x16x32_bf16 v[10:13], v[160:163], v[192:195], v[10:13]
	v_mfma_f32_16x16x32_bf16 v[62:65], v[156:159], v[172:175], v[62:65]
	v_mfma_f32_16x16x32_bf16 v[58:61], v[164:167], v[172:175], v[58:61]
	v_mfma_f32_16x16x32_bf16 v[46:49], v[156:159], v[180:183], v[46:49]
	v_mfma_f32_16x16x32_bf16 v[42:45], v[164:167], v[180:183], v[42:45]
	v_mfma_f32_16x16x32_bf16 v[30:33], v[156:159], v[188:191], v[30:33]
	v_mfma_f32_16x16x32_bf16 v[26:29], v[164:167], v[188:191], v[26:29]
	v_mfma_f32_16x16x32_bf16 v[14:17], v[156:159], v[196:199], v[14:17]
	v_mfma_f32_16x16x32_bf16 v[10:13], v[164:167], v[196:199], v[10:13]
	s_setprio 0
	s_barrier
	s_add_u32 s56, s24, 0x40000
	s_addc_u32 s57, s25, 0
	s_add_i32 s55, s46, s36
	v_lshl_add_u64 v[142:143], s[56:57], 0, v[130:131]
	s_mov_b32 m0, s55
	s_nop 0
	global_load_lds_dwordx4 v[142:143], off
	v_lshl_add_u64 v[142:143], s[56:57], 0, v[132:133]
	s_add_i32 m0, s55, 0x2000
	s_nop 0
	global_load_lds_dwordx4 v[142:143], off
	s_waitcnt vmcnt(6)
	s_barrier
	s_setprio 1
	v_mfma_f32_16x16x32_bf16 v[54:57], v[200:203], v[168:171], v[54:57]
	v_mfma_f32_16x16x32_bf16 v[50:53], v[208:211], v[168:171], v[50:53]
	v_mfma_f32_16x16x32_bf16 v[38:41], v[200:203], v[176:179], v[38:41]
	v_mfma_f32_16x16x32_bf16 v[34:37], v[208:211], v[176:179], v[34:37]
	v_mfma_f32_16x16x32_bf16 v[22:25], v[200:203], v[184:187], v[22:25]
	v_mfma_f32_16x16x32_bf16 v[18:21], v[208:211], v[184:187], v[18:21]
	v_mfma_f32_16x16x32_bf16 v[6:9], v[200:203], v[192:195], v[6:9]
	v_mfma_f32_16x16x32_bf16 v[2:5], v[208:211], v[192:195], v[2:5]
	v_mfma_f32_16x16x32_bf16 v[54:57], v[204:207], v[172:175], v[54:57]
	v_mfma_f32_16x16x32_bf16 v[50:53], v[212:215], v[172:175], v[50:53]
	v_mfma_f32_16x16x32_bf16 v[38:41], v[204:207], v[180:183], v[38:41]
	v_mfma_f32_16x16x32_bf16 v[34:37], v[212:215], v[180:183], v[34:37]
	v_mfma_f32_16x16x32_bf16 v[22:25], v[204:207], v[188:191], v[22:25]
	v_mfma_f32_16x16x32_bf16 v[18:21], v[212:215], v[188:191], v[18:21]
	v_mfma_f32_16x16x32_bf16 v[6:9], v[204:207], v[196:199], v[6:9]
	v_mfma_f32_16x16x32_bf16 v[2:5], v[212:215], v[196:199], v[2:5]
	s_setprio 0
	s_add_i32 s55, 0, 0x18000
	v_add_u32_e32 v150, s55, v152
	s_barrier
	ds_read_b128 v[142:145], v150
	ds_read_b128 v[156:159], v150 offset:1024
	ds_read_b128 v[160:163], v150 offset:2048
	ds_read_b128 v[164:167], v150 offset:3072
	s_add_u32 s26, s26, 0x40000
	s_addc_u32 s27, s27, 0
	s_mov_b32 m0, s39
	v_lshl_add_u64 v[200:201], s[26:27], 0, v[130:131]
	ds_read_b128 v[168:171], v148 offset:32768
	ds_read_b128 v[172:175], v148 offset:33792
	ds_read_b128 v[176:179], v148 offset:34816
	ds_read_b128 v[180:183], v148 offset:35840
	ds_read_b128 v[184:187], v148 offset:36864
	ds_read_b128 v[188:191], v148 offset:37888
	ds_read_b128 v[192:195], v148 offset:38912
	ds_read_b128 v[196:199], v148 offset:39936
	global_load_lds_dwordx4 v[200:201], off
	v_lshl_add_u64 v[200:201], s[26:27], 0, v[132:133]
	s_mov_b32 m0, s40
	s_nop 0
	global_load_lds_dwordx4 v[200:201], off
	s_waitcnt lgkmcnt(8)
	s_barrier
	s_waitcnt lgkmcnt(0)
	s_setprio 1
	s_waitcnt lgkmcnt(0)
	v_mfma_f32_16x16x32_bf16 v[126:129], v[142:145], v[168:171], v[126:129]
	v_mfma_f32_16x16x32_bf16 v[122:125], v[160:163], v[168:171], v[122:125]
	v_mfma_f32_16x16x32_bf16 v[110:113], v[142:145], v[176:179], v[110:113]
	v_mfma_f32_16x16x32_bf16 v[106:109], v[160:163], v[176:179], v[106:109]
	v_mfma_f32_16x16x32_bf16 v[94:97], v[142:145], v[184:187], v[94:97]
	v_mfma_f32_16x16x32_bf16 v[90:93], v[160:163], v[184:187], v[90:93]
	v_mfma_f32_16x16x32_bf16 v[78:81], v[142:145], v[192:195], v[78:81]
	v_mfma_f32_16x16x32_bf16 v[74:77], v[160:163], v[192:195], v[74:77]
	v_mfma_f32_16x16x32_bf16 v[126:129], v[156:159], v[172:175], v[126:129]
	v_mfma_f32_16x16x32_bf16 v[122:125], v[164:167], v[172:175], v[122:125]
	v_mfma_f32_16x16x32_bf16 v[110:113], v[156:159], v[180:183], v[110:113]
	v_mfma_f32_16x16x32_bf16 v[106:109], v[164:167], v[180:183], v[106:109]
	v_mfma_f32_16x16x32_bf16 v[94:97], v[156:159], v[188:191], v[94:97]
	v_mfma_f32_16x16x32_bf16 v[90:93], v[164:167], v[188:191], v[90:93]
	v_mfma_f32_16x16x32_bf16 v[78:81], v[156:159], v[196:199], v[78:81]
	v_mfma_f32_16x16x32_bf16 v[74:77], v[164:167], v[196:199], v[74:77]
	s_setprio 0
	s_barrier
	s_add_i32 s26, 0, 0x1c000
	s_add_i32 s27, s55, s36
	v_add_u32_e32 v150, s26, v152
	v_lshl_add_u64 v[146:147], v[146:147], 0, s[2:3]
	s_mov_b32 m0, s27
	ds_read_b128 v[200:203], v150
	ds_read_b128 v[204:207], v150 offset:1024
	ds_read_b128 v[208:211], v150 offset:2048
	ds_read_b128 v[212:215], v150 offset:3072
	global_load_lds_dwordx4 v[146:147], off
	v_lshl_add_u64 v[146:147], v[216:217], 0, s[2:3]
	s_add_i32 m0, s27, 0x2000
	s_nop 0
	global_load_lds_dwordx4 v[146:147], off
	s_barrier
	s_waitcnt lgkmcnt(0)
	s_setprio 1
	s_waitcnt lgkmcnt(0)
	v_mfma_f32_16x16x32_bf16 v[118:121], v[200:203], v[168:171], v[118:121]
	v_mfma_f32_16x16x32_bf16 v[114:117], v[208:211], v[168:171], v[114:117]
	v_mfma_f32_16x16x32_bf16 v[102:105], v[200:203], v[176:179], v[102:105]
	v_mfma_f32_16x16x32_bf16 v[98:101], v[208:211], v[176:179], v[98:101]
	v_mfma_f32_16x16x32_bf16 v[86:89], v[200:203], v[184:187], v[86:89]
	v_mfma_f32_16x16x32_bf16 v[82:85], v[208:211], v[184:187], v[82:85]
	v_mfma_f32_16x16x32_bf16 v[70:73], v[200:203], v[192:195], v[70:73]
	v_mfma_f32_16x16x32_bf16 v[66:69], v[208:211], v[192:195], v[66:69]
	v_mfma_f32_16x16x32_bf16 v[118:121], v[204:207], v[172:175], v[118:121]
	v_mfma_f32_16x16x32_bf16 v[114:117], v[212:215], v[172:175], v[114:117]
	v_mfma_f32_16x16x32_bf16 v[102:105], v[204:207], v[180:183], v[102:105]
	v_mfma_f32_16x16x32_bf16 v[98:101], v[212:215], v[180:183], v[98:101]
	v_mfma_f32_16x16x32_bf16 v[86:89], v[204:207], v[188:191], v[86:89]
	v_mfma_f32_16x16x32_bf16 v[82:85], v[212:215], v[188:191], v[82:85]
	v_mfma_f32_16x16x32_bf16 v[70:73], v[204:207], v[196:199], v[70:73]
	v_mfma_f32_16x16x32_bf16 v[66:69], v[212:215], v[196:199], v[66:69]
	s_setprio 0
	s_mov_b32 m0, s42
	v_lshl_add_u64 v[146:147], v[218:219], 0, s[2:3]
	s_barrier
	ds_read_b128 v[168:171], v148 offset:49152
	ds_read_b128 v[172:175], v148 offset:50176
	ds_read_b128 v[176:179], v148 offset:51200
	ds_read_b128 v[180:183], v148 offset:52224
	ds_read_b128 v[184:187], v148 offset:53248
	ds_read_b128 v[188:191], v148 offset:54272
	ds_read_b128 v[192:195], v148 offset:55296
	ds_read_b128 v[196:199], v148 offset:56320
	global_load_lds_dwordx4 v[146:147], off
	v_lshl_add_u64 v[146:147], v[220:221], 0, s[2:3]
	s_mov_b32 m0, s43
	s_nop 0
	global_load_lds_dwordx4 v[146:147], off
	s_barrier
	s_waitcnt lgkmcnt(0)
	s_setprio 1
	s_waitcnt lgkmcnt(0)
	v_mfma_f32_16x16x32_bf16 v[62:65], v[142:145], v[168:171], v[62:65]
	v_mfma_f32_16x16x32_bf16 v[58:61], v[160:163], v[168:171], v[58:61]
	v_mfma_f32_16x16x32_bf16 v[46:49], v[142:145], v[176:179], v[46:49]
	v_mfma_f32_16x16x32_bf16 v[42:45], v[160:163], v[176:179], v[42:45]
	v_mfma_f32_16x16x32_bf16 v[30:33], v[142:145], v[184:187], v[30:33]
	v_mfma_f32_16x16x32_bf16 v[26:29], v[160:163], v[184:187], v[26:29]
	v_mfma_f32_16x16x32_bf16 v[14:17], v[142:145], v[192:195], v[14:17]
	v_mfma_f32_16x16x32_bf16 v[10:13], v[160:163], v[192:195], v[10:13]
	v_mfma_f32_16x16x32_bf16 v[62:65], v[156:159], v[172:175], v[62:65]
	v_mfma_f32_16x16x32_bf16 v[58:61], v[164:167], v[172:175], v[58:61]
	v_mfma_f32_16x16x32_bf16 v[46:49], v[156:159], v[180:183], v[46:49]
	v_mfma_f32_16x16x32_bf16 v[42:45], v[164:167], v[180:183], v[42:45]
	v_mfma_f32_16x16x32_bf16 v[30:33], v[156:159], v[188:191], v[30:33]
	v_mfma_f32_16x16x32_bf16 v[26:29], v[164:167], v[188:191], v[26:29]
	v_mfma_f32_16x16x32_bf16 v[14:17], v[156:159], v[196:199], v[14:17]
	v_mfma_f32_16x16x32_bf16 v[10:13], v[164:167], v[196:199], v[10:13]
	s_setprio 0
	s_barrier
	s_add_u32 s24, s24, 0x40080
	s_addc_u32 s25, s25, 0
	s_add_i32 s26, s26, s36
	v_lshl_add_u64 v[142:143], s[24:25], 0, v[130:131]
	s_mov_b32 m0, s26
	s_nop 0
	global_load_lds_dwordx4 v[142:143], off
	v_lshl_add_u64 v[142:143], s[24:25], 0, v[132:133]
	s_add_i32 m0, s26, 0x2000
	s_nop 0
	global_load_lds_dwordx4 v[142:143], off
	s_waitcnt vmcnt(6)
	s_barrier
	s_setprio 1
	v_mfma_f32_16x16x32_bf16 v[54:57], v[200:203], v[168:171], v[54:57]
	v_mfma_f32_16x16x32_bf16 v[50:53], v[208:211], v[168:171], v[50:53]
	v_mfma_f32_16x16x32_bf16 v[38:41], v[200:203], v[176:179], v[38:41]
	v_mfma_f32_16x16x32_bf16 v[34:37], v[208:211], v[176:179], v[34:37]
	v_mfma_f32_16x16x32_bf16 v[22:25], v[200:203], v[184:187], v[22:25]
	v_mfma_f32_16x16x32_bf16 v[18:21], v[208:211], v[184:187], v[18:21]
	v_mfma_f32_16x16x32_bf16 v[6:9], v[200:203], v[192:195], v[6:9]
	v_mfma_f32_16x16x32_bf16 v[2:5], v[208:211], v[192:195], v[2:5]
	v_mfma_f32_16x16x32_bf16 v[54:57], v[204:207], v[172:175], v[54:57]
	v_mfma_f32_16x16x32_bf16 v[50:53], v[212:215], v[172:175], v[50:53]
	v_mfma_f32_16x16x32_bf16 v[38:41], v[204:207], v[180:183], v[38:41]
	v_mfma_f32_16x16x32_bf16 v[34:37], v[212:215], v[180:183], v[34:37]
	v_mfma_f32_16x16x32_bf16 v[22:25], v[204:207], v[188:191], v[22:25]
	v_mfma_f32_16x16x32_bf16 v[18:21], v[212:215], v[188:191], v[18:21]
	v_mfma_f32_16x16x32_bf16 v[6:9], v[204:207], v[196:199], v[6:9]
	v_mfma_f32_16x16x32_bf16 v[2:5], v[212:215], v[196:199], v[2:5]
	s_setprio 0
	s_add_i32 s54, s54, 2
	s_add_u32 s22, s22, 0x100
	s_addc_u32 s23, s23, 0
	s_add_u32 s52, s52, 0x100
	s_addc_u32 s53, s53, 0
	s_cmp_gt_u32 s54, 13
	s_barrier
	s_cbranch_scc0 .LBB0_3255
	v_lshl_or_b32 v142, s49, 8, v151
	v_lshl_add_u32 v144, s20, 8, v155
	v_ashrrev_i32_e32 v143, 31, v142
	v_mov_b64_e32 v[146:147], s[6:7]
	v_ashrrev_i32_e32 v145, 31, v144
	v_mad_i64_i32 v[156:157], s[22:23], v144, s47, v[146:147]
	v_lshlrev_b64 v[142:143], 1, v[142:143]
	v_lshl_add_u64 v[156:157], v[156:157], 0, v[142:143]
	v_lshlrev_b64 v[160:161], 12, v[144:145]
	v_add_co_u32_e32 v158, vcc, 0x2ec42000, v156
	v_lshl_add_u64 v[160:161], s[8:9], 0, v[160:161]
	s_nop 0
	v_addc_co_u32_e32 v159, vcc, 0, v157, vcc
	v_lshl_add_u64 v[160:161], v[160:161], 0, v[142:143]
	v_mov_b32_e32 v228, v158
	v_mov_b32_e32 v229, v159
	v_mov_b32_e32 v232, v160
	v_mov_b32_e32 v233, v161
	v_mov_b32_e32 v237, 0x1000
	global_load_dwordx2 v[168:169], v[228:229], off
	global_load_dwordx2 v[170:171], v[232:233], off
	global_load_dwordx2 v[172:173], v[228:229], off offset:32
	global_load_dwordx2 v[174:175], v[232:233], off offset:32
	global_load_dwordx2 v[176:177], v[228:229], off offset:256
	global_load_dwordx2 v[178:179], v[232:233], off offset:256
	global_load_dwordx2 v[180:181], v[228:229], off offset:288
	global_load_dwordx2 v[182:183], v[232:233], off offset:288
	v_mov_b32_e32 v236, 16
	v_mad_i64_i32 v[230:231], s[22:23], v236, s47, v[228:229]
	v_mad_i64_i32 v[234:235], s[22:23], v236, v237, v[232:233]
	global_load_dwordx2 v[184:185], v[230:231], off
	global_load_dwordx2 v[186:187], v[234:235], off
	global_load_dwordx2 v[188:189], v[230:231], off offset:32
	global_load_dwordx2 v[190:191], v[234:235], off offset:32
	global_load_dwordx2 v[192:193], v[230:231], off offset:256
	global_load_dwordx2 v[194:195], v[234:235], off offset:256
	global_load_dwordx2 v[196:197], v[230:231], off offset:288
	global_load_dwordx2 v[198:199], v[234:235], off offset:288
	v_mov_b32_e32 v236, 32
	v_mad_i64_i32 v[230:231], s[22:23], v236, s47, v[228:229]
	v_mad_i64_i32 v[234:235], s[22:23], v236, v237, v[232:233]
	global_load_dwordx2 v[200:201], v[230:231], off
	global_load_dwordx2 v[202:203], v[234:235], off
	global_load_dwordx2 v[204:205], v[230:231], off offset:32
	global_load_dwordx2 v[206:207], v[234:235], off offset:32
	global_load_dwordx2 v[208:209], v[230:231], off offset:256
	global_load_dwordx2 v[210:211], v[234:235], off offset:256
	global_load_dwordx2 v[212:213], v[230:231], off offset:288
	global_load_dwordx2 v[214:215], v[234:235], off offset:288
	s_waitcnt vmcnt(0)
	v_mov_b32_e32 v158, v168
	v_mov_b32_e32 v159, v169
	v_lshl_add_u64 v[156:157], v[156:157], 0, s[10:11]
	v_mov_b32_e32 v162, v170
	v_mov_b32_e32 v163, v171
	s_mov_b32 s49, s12
	s_mov_b32 s20, s14
	s_mov_b64 s[24:25], s[18:19]
	s_nop 0
	v_lshlrev_b32_e32 v164, 16, v158
	v_and_b32_e32 v165, 0xffff0000, v158
	v_lshlrev_b32_e32 v158, 16, v159
	v_and_b32_e32 v159, 0xffff0000, v159
	v_lshlrev_b32_e32 v166, 16, v162
	v_and_b32_e32 v167, 0xffff0000, v162
	v_lshlrev_b32_e32 v162, 16, v163
	v_and_b32_e32 v163, 0xffff0000, v163
	v_pk_fma_f32 v[128:129], v[128:129], v[158:159], v[162:163]
	v_pk_fma_f32 v[126:127], v[126:127], v[164:165], v[166:167]
	s_nop 0
	v_cvt_pk_bf16_f32 v126, v126, v127
	v_cvt_pk_bf16_f32 v127, v128, v129
	v_mov_b32_e32 v128, v172
	v_mov_b32_e32 v129, v173
	v_mov_b32_e32 v158, v174
	v_mov_b32_e32 v159, v175
	s_nop 0
	v_lshlrev_b32_e32 v162, 16, v158
	global_store_dwordx2 v[160:161], v[126:127], off
	v_lshlrev_b32_e32 v126, 16, v128
	v_and_b32_e32 v127, 0xffff0000, v128
	v_lshlrev_b32_e32 v128, 16, v129
	v_and_b32_e32 v129, 0xffff0000, v129
	v_and_b32_e32 v163, 0xffff0000, v158
	v_lshlrev_b32_e32 v158, 16, v159
	v_and_b32_e32 v159, 0xffff0000, v159
	v_pk_fma_f32 v[124:125], v[124:125], v[128:129], v[158:159]
	v_pk_fma_f32 v[122:123], v[122:123], v[126:127], v[162:163]
	s_nop 0
	v_cvt_pk_bf16_f32 v122, v122, v123
	v_cvt_pk_bf16_f32 v123, v124, v125
	v_mov_b32_e32 v124, v176
	v_mov_b32_e32 v125, v177
	v_mov_b32_e32 v126, v178
	v_mov_b32_e32 v127, v179
	s_nop 0
	v_lshlrev_b32_e32 v128, 16, v126
	global_store_dwordx2 v[160:161], v[122:123], off offset:32
	v_lshlrev_b32_e32 v122, 16, v124
	v_and_b32_e32 v123, 0xffff0000, v124
	v_lshlrev_b32_e32 v124, 16, v125
	v_and_b32_e32 v125, 0xffff0000, v125
	v_and_b32_e32 v129, 0xffff0000, v126
	v_lshlrev_b32_e32 v126, 16, v127
	v_and_b32_e32 v127, 0xffff0000, v127
	v_pk_fma_f32 v[120:121], v[120:121], v[124:125], v[126:127]
	v_pk_fma_f32 v[118:119], v[118:119], v[122:123], v[128:129]
	v_or_b32_e32 v124, 16, v144
	v_cvt_pk_bf16_f32 v118, v118, v119
	v_cvt_pk_bf16_f32 v119, v120, v121
	v_mov_b32_e32 v120, v180
	v_mov_b32_e32 v121, v181
	v_mov_b32_e32 v122, v182
	v_mov_b32_e32 v123, v183
	v_ashrrev_i32_e32 v125, 31, v124
	v_mad_i64_i32 v[126:127], s[22:23], v124, s47, v[146:147]
	global_store_dwordx2 v[160:161], v[118:119], off offset:256
	v_lshl_add_u64 v[126:127], v[126:127], 0, v[142:143]
	v_add_co_u32_e32 v128, vcc, s48, v126
	s_nop 0
	v_lshlrev_b32_e32 v118, 16, v120
	v_and_b32_e32 v119, 0xffff0000, v120
	v_lshlrev_b32_e32 v156, 16, v122
	v_and_b32_e32 v157, 0xffff0000, v122
	v_pk_fma_f32 v[114:115], v[114:115], v[118:119], v[156:157]
	v_lshlrev_b64 v[118:119], 12, v[124:125]
	v_lshlrev_b32_e32 v120, 16, v121
	v_and_b32_e32 v121, 0xffff0000, v121
	v_lshlrev_b32_e32 v122, 16, v123
	v_and_b32_e32 v123, 0xffff0000, v123
	v_lshl_add_u64 v[118:119], s[8:9], 0, v[118:119]
	v_addc_co_u32_e32 v129, vcc, 0, v127, vcc
	v_pk_fma_f32 v[116:117], v[116:117], v[120:121], v[122:123]
	v_lshl_add_u64 v[118:119], v[118:119], 0, v[142:143]
	v_cvt_pk_bf16_f32 v114, v114, v115
	v_cvt_pk_bf16_f32 v115, v116, v117
	v_mov_b32_e32 v116, v184
	v_mov_b32_e32 v117, v185
	v_mov_b32_e32 v120, v186
	v_mov_b32_e32 v121, v187
	v_lshl_add_u64 v[122:123], v[126:127], 0, s[10:11]
	global_store_dwordx2 v[160:161], v[114:115], off offset:288
	s_nop 0
	v_lshlrev_b32_e32 v114, 16, v116
	v_and_b32_e32 v115, 0xffff0000, v116
	v_lshlrev_b32_e32 v116, 16, v117
	v_and_b32_e32 v117, 0xffff0000, v117
	v_lshlrev_b32_e32 v124, 16, v120
	v_and_b32_e32 v125, 0xffff0000, v120
	v_lshlrev_b32_e32 v120, 16, v121
	v_and_b32_e32 v121, 0xffff0000, v121
	v_pk_fma_f32 v[112:113], v[112:113], v[116:117], v[120:121]
	v_pk_fma_f32 v[110:111], v[110:111], v[114:115], v[124:125]
	s_nop 0
	v_cvt_pk_bf16_f32 v110, v110, v111
	v_cvt_pk_bf16_f32 v111, v112, v113
	v_mov_b32_e32 v112, v188
	v_mov_b32_e32 v113, v189
	v_mov_b32_e32 v114, v190
	v_mov_b32_e32 v115, v191
	s_nop 0
	v_lshlrev_b32_e32 v116, 16, v114
	global_store_dwordx2 v[118:119], v[110:111], off
	v_lshlrev_b32_e32 v110, 16, v112
	v_and_b32_e32 v111, 0xffff0000, v112
	v_lshlrev_b32_e32 v112, 16, v113
	v_and_b32_e32 v113, 0xffff0000, v113
	v_and_b32_e32 v117, 0xffff0000, v114
	v_lshlrev_b32_e32 v114, 16, v115
	v_and_b32_e32 v115, 0xffff0000, v115
	v_pk_fma_f32 v[108:109], v[108:109], v[112:113], v[114:115]
	v_pk_fma_f32 v[106:107], v[106:107], v[110:111], v[116:117]
	s_nop 0
	v_cvt_pk_bf16_f32 v106, v106, v107
	v_cvt_pk_bf16_f32 v107, v108, v109
	v_mov_b32_e32 v108, v192
	v_mov_b32_e32 v109, v193
	v_mov_b32_e32 v110, v194
	v_mov_b32_e32 v111, v195
	s_nop 0
	v_lshlrev_b32_e32 v112, 16, v110
	global_store_dwordx2 v[118:119], v[106:107], off offset:32
	v_lshlrev_b32_e32 v106, 16, v108
	v_and_b32_e32 v107, 0xffff0000, v108
	v_lshlrev_b32_e32 v108, 16, v109
	v_and_b32_e32 v109, 0xffff0000, v109
	v_and_b32_e32 v113, 0xffff0000, v110
	v_lshlrev_b32_e32 v110, 16, v111
	v_and_b32_e32 v111, 0xffff0000, v111
	v_pk_fma_f32 v[104:105], v[104:105], v[108:109], v[110:111]
	v_pk_fma_f32 v[102:103], v[102:103], v[106:107], v[112:113]
	v_or_b32_e32 v108, 32, v144
	v_cvt_pk_bf16_f32 v102, v102, v103
	v_cvt_pk_bf16_f32 v103, v104, v105
	v_mov_b32_e32 v104, v196
	v_mov_b32_e32 v105, v197
	v_mov_b32_e32 v106, v198
	v_mov_b32_e32 v107, v199
	v_ashrrev_i32_e32 v109, 31, v108
	v_mad_i64_i32 v[110:111], s[22:23], v108, s47, v[146:147]
	global_store_dwordx2 v[118:119], v[102:103], off offset:256
	v_lshl_add_u64 v[110:111], v[110:111], 0, v[142:143]
	v_add_co_u32_e32 v112, vcc, s48, v110
	s_nop 0
	v_lshlrev_b32_e32 v102, 16, v104
	v_and_b32_e32 v103, 0xffff0000, v104
	v_lshlrev_b32_e32 v114, 16, v106
	v_and_b32_e32 v115, 0xffff0000, v106
	v_pk_fma_f32 v[98:99], v[98:99], v[102:103], v[114:115]
	v_lshlrev_b64 v[102:103], 12, v[108:109]
	v_lshlrev_b32_e32 v104, 16, v105
	v_and_b32_e32 v105, 0xffff0000, v105
	v_lshlrev_b32_e32 v106, 16, v107
	v_and_b32_e32 v107, 0xffff0000, v107
	v_lshl_add_u64 v[102:103], s[8:9], 0, v[102:103]
	v_addc_co_u32_e32 v113, vcc, 0, v111, vcc
	v_pk_fma_f32 v[100:101], v[100:101], v[104:105], v[106:107]
	v_lshl_add_u64 v[102:103], v[102:103], 0, v[142:143]
	v_cvt_pk_bf16_f32 v98, v98, v99
	v_cvt_pk_bf16_f32 v99, v100, v101
	v_mov_b32_e32 v100, v200
	v_mov_b32_e32 v101, v201
	v_mov_b32_e32 v104, v202
	v_mov_b32_e32 v105, v203
	v_lshl_add_u64 v[106:107], v[110:111], 0, s[10:11]
	global_store_dwordx2 v[118:119], v[98:99], off offset:288
	s_nop 0
	v_lshlrev_b32_e32 v98, 16, v100
	v_and_b32_e32 v99, 0xffff0000, v100
	v_lshlrev_b32_e32 v100, 16, v101
	v_and_b32_e32 v101, 0xffff0000, v101
	v_lshlrev_b32_e32 v108, 16, v104
	v_and_b32_e32 v109, 0xffff0000, v104
	v_lshlrev_b32_e32 v104, 16, v105
	v_and_b32_e32 v105, 0xffff0000, v105
	v_pk_fma_f32 v[96:97], v[96:97], v[100:101], v[104:105]
	v_pk_fma_f32 v[94:95], v[94:95], v[98:99], v[108:109]
	s_nop 0
	v_cvt_pk_bf16_f32 v94, v94, v95
	v_cvt_pk_bf16_f32 v95, v96, v97
	v_mov_b32_e32 v96, v204
	v_mov_b32_e32 v97, v205
	v_mov_b32_e32 v98, v206
	v_mov_b32_e32 v99, v207
	s_nop 0
	v_lshlrev_b32_e32 v100, 16, v98
	global_store_dwordx2 v[102:103], v[94:95], off
	v_lshlrev_b32_e32 v94, 16, v96
	v_and_b32_e32 v95, 0xffff0000, v96
	v_lshlrev_b32_e32 v96, 16, v97
	v_and_b32_e32 v97, 0xffff0000, v97
	v_and_b32_e32 v101, 0xffff0000, v98
	v_lshlrev_b32_e32 v98, 16, v99
	v_and_b32_e32 v99, 0xffff0000, v99
	v_pk_fma_f32 v[92:93], v[92:93], v[96:97], v[98:99]
	v_pk_fma_f32 v[90:91], v[90:91], v[94:95], v[100:101]
	s_nop 0
	v_cvt_pk_bf16_f32 v90, v90, v91
	v_cvt_pk_bf16_f32 v91, v92, v93
	v_mov_b32_e32 v92, v208
	v_mov_b32_e32 v93, v209
	v_mov_b32_e32 v94, v210
	v_mov_b32_e32 v95, v211
	s_nop 0
	v_lshlrev_b32_e32 v96, 16, v94
	global_store_dwordx2 v[102:103], v[90:91], off offset:32
	v_lshlrev_b32_e32 v90, 16, v92
	v_and_b32_e32 v91, 0xffff0000, v92
	v_lshlrev_b32_e32 v92, 16, v93
	v_and_b32_e32 v93, 0xffff0000, v93
	v_and_b32_e32 v97, 0xffff0000, v94
	v_lshlrev_b32_e32 v94, 16, v95
	v_and_b32_e32 v95, 0xffff0000, v95
	v_pk_fma_f32 v[88:89], v[88:89], v[92:93], v[94:95]
	v_pk_fma_f32 v[86:87], v[86:87], v[90:91], v[96:97]
	v_or_b32_e32 v92, 48, v144
	v_cvt_pk_bf16_f32 v86, v86, v87
	v_cvt_pk_bf16_f32 v87, v88, v89
	v_mov_b32_e32 v88, v212
	v_mov_b32_e32 v89, v213
	v_mov_b32_e32 v90, v214
	v_mov_b32_e32 v91, v215
	v_ashrrev_i32_e32 v93, 31, v92
	v_mad_i64_i32 v[94:95], s[22:23], v92, s47, v[146:147]
	global_store_dwordx2 v[102:103], v[86:87], off offset:256
	v_lshl_add_u64 v[94:95], v[94:95], 0, v[142:143]
	v_add_co_u32_e32 v96, vcc, s48, v94
	s_nop 0
	v_lshlrev_b32_e32 v86, 16, v88
	v_and_b32_e32 v87, 0xffff0000, v88
	v_lshlrev_b32_e32 v98, 16, v90
	v_and_b32_e32 v99, 0xffff0000, v90
	v_pk_fma_f32 v[82:83], v[82:83], v[86:87], v[98:99]
	v_lshlrev_b64 v[86:87], 12, v[92:93]
	v_lshlrev_b32_e32 v88, 16, v89
	v_and_b32_e32 v89, 0xffff0000, v89
	v_lshlrev_b32_e32 v90, 16, v91
	v_and_b32_e32 v91, 0xffff0000, v91
	v_lshl_add_u64 v[86:87], s[8:9], 0, v[86:87]
	v_addc_co_u32_e32 v97, vcc, 0, v95, vcc
	v_pk_fma_f32 v[84:85], v[84:85], v[88:89], v[90:91]
	v_lshl_add_u64 v[86:87], v[86:87], 0, v[142:143]
	v_cvt_pk_bf16_f32 v82, v82, v83
	v_cvt_pk_bf16_f32 v83, v84, v85
	v_mov_b32_e32 v237, 0x1000
	v_mov_b32_e32 v236, 48
	v_mad_i64_i32 v[230:231], s[22:23], v236, s47, v[228:229]
	v_mad_i64_i32 v[234:235], s[22:23], v236, v237, v[232:233]
	global_load_dwordx2 v[168:169], v[230:231], off
	global_load_dwordx2 v[170:171], v[234:235], off
	global_load_dwordx2 v[172:173], v[230:231], off offset:32
	global_load_dwordx2 v[174:175], v[234:235], off offset:32
	global_load_dwordx2 v[176:177], v[230:231], off offset:256
	global_load_dwordx2 v[178:179], v[234:235], off offset:256
	global_load_dwordx2 v[180:181], v[230:231], off offset:288
	global_load_dwordx2 v[182:183], v[234:235], off offset:288
	v_mov_b32_e32 v236, 128
	v_mad_i64_i32 v[230:231], s[22:23], v236, s47, v[228:229]
	v_mad_i64_i32 v[234:235], s[22:23], v236, v237, v[232:233]
	global_load_dwordx2 v[184:185], v[230:231], off
	global_load_dwordx2 v[186:187], v[234:235], off
	global_load_dwordx2 v[188:189], v[230:231], off offset:32
	global_load_dwordx2 v[190:191], v[234:235], off offset:32
	global_load_dwordx2 v[192:193], v[230:231], off offset:256
	global_load_dwordx2 v[194:195], v[234:235], off offset:256
	global_load_dwordx2 v[196:197], v[230:231], off offset:288
	global_load_dwordx2 v[198:199], v[234:235], off offset:288
	v_mov_b32_e32 v236, 144
	v_mad_i64_i32 v[230:231], s[22:23], v236, s47, v[228:229]
	v_mad_i64_i32 v[234:235], s[22:23], v236, v237, v[232:233]
	global_load_dwordx2 v[200:201], v[230:231], off
	global_load_dwordx2 v[202:203], v[234:235], off
	global_load_dwordx2 v[204:205], v[230:231], off offset:32
	global_load_dwordx2 v[206:207], v[234:235], off offset:32
	global_load_dwordx2 v[208:209], v[230:231], off offset:256
	global_load_dwordx2 v[210:211], v[234:235], off offset:256
	global_load_dwordx2 v[212:213], v[230:231], off offset:288
	global_load_dwordx2 v[214:215], v[234:235], off offset:288
	s_waitcnt vmcnt(0)
	v_mov_b32_e32 v84, v168
	v_mov_b32_e32 v85, v169
	v_mov_b32_e32 v88, v170
	v_mov_b32_e32 v89, v171
	v_lshl_add_u64 v[90:91], v[94:95], 0, s[10:11]
	global_store_dwordx2 v[102:103], v[82:83], off offset:288
	s_nop 0
	v_lshlrev_b32_e32 v82, 16, v84
	v_and_b32_e32 v83, 0xffff0000, v84
	v_lshlrev_b32_e32 v84, 16, v85
	v_and_b32_e32 v85, 0xffff0000, v85
	v_lshlrev_b32_e32 v92, 16, v88
	v_and_b32_e32 v93, 0xffff0000, v88
	v_lshlrev_b32_e32 v88, 16, v89
	v_and_b32_e32 v89, 0xffff0000, v89
	v_pk_fma_f32 v[80:81], v[80:81], v[84:85], v[88:89]
	v_pk_fma_f32 v[78:79], v[78:79], v[82:83], v[92:93]
	s_nop 0
	v_cvt_pk_bf16_f32 v78, v78, v79
	v_cvt_pk_bf16_f32 v79, v80, v81
	v_mov_b32_e32 v80, v172
	v_mov_b32_e32 v81, v173
	v_mov_b32_e32 v82, v174
	v_mov_b32_e32 v83, v175
	s_nop 0
	v_lshlrev_b32_e32 v84, 16, v82
	global_store_dwordx2 v[86:87], v[78:79], off
	v_lshlrev_b32_e32 v78, 16, v80
	v_and_b32_e32 v79, 0xffff0000, v80
	v_lshlrev_b32_e32 v80, 16, v81
	v_and_b32_e32 v81, 0xffff0000, v81
	v_and_b32_e32 v85, 0xffff0000, v82
	v_lshlrev_b32_e32 v82, 16, v83
	v_and_b32_e32 v83, 0xffff0000, v83
	v_pk_fma_f32 v[76:77], v[76:77], v[80:81], v[82:83]
	v_pk_fma_f32 v[74:75], v[74:75], v[78:79], v[84:85]
	s_nop 0
	v_cvt_pk_bf16_f32 v74, v74, v75
	v_cvt_pk_bf16_f32 v75, v76, v77
	v_mov_b32_e32 v76, v176
	v_mov_b32_e32 v77, v177
	v_mov_b32_e32 v78, v178
	v_mov_b32_e32 v79, v179
	s_nop 0
	v_lshlrev_b32_e32 v80, 16, v78
	global_store_dwordx2 v[86:87], v[74:75], off offset:32
	v_lshlrev_b32_e32 v74, 16, v76
	v_and_b32_e32 v75, 0xffff0000, v76
	v_lshlrev_b32_e32 v76, 16, v77
	v_and_b32_e32 v77, 0xffff0000, v77
	v_and_b32_e32 v81, 0xffff0000, v78
	v_lshlrev_b32_e32 v78, 16, v79
	v_and_b32_e32 v79, 0xffff0000, v79
	v_pk_fma_f32 v[72:73], v[72:73], v[76:77], v[78:79]
	v_pk_fma_f32 v[70:71], v[70:71], v[74:75], v[80:81]
	v_add_u32_e32 v76, 0x80, v144
	v_cvt_pk_bf16_f32 v70, v70, v71
	v_cvt_pk_bf16_f32 v71, v72, v73
	v_mov_b32_e32 v72, v180
	v_mov_b32_e32 v73, v181
	v_mov_b32_e32 v74, v182
	v_mov_b32_e32 v75, v183
	v_ashrrev_i32_e32 v77, 31, v76
	v_mad_i64_i32 v[78:79], s[22:23], v76, s47, v[146:147]
	global_store_dwordx2 v[86:87], v[70:71], off offset:256
	v_lshl_add_u64 v[78:79], v[78:79], 0, v[142:143]
	v_add_co_u32_e32 v80, vcc, s48, v78
	s_nop 0
	v_lshlrev_b32_e32 v70, 16, v72
	v_and_b32_e32 v71, 0xffff0000, v72
	v_lshlrev_b32_e32 v82, 16, v74
	v_and_b32_e32 v83, 0xffff0000, v74
	v_pk_fma_f32 v[66:67], v[66:67], v[70:71], v[82:83]
	v_lshlrev_b64 v[70:71], 12, v[76:77]
	v_lshlrev_b32_e32 v72, 16, v73
	v_and_b32_e32 v73, 0xffff0000, v73
	v_lshlrev_b32_e32 v74, 16, v75
	v_and_b32_e32 v75, 0xffff0000, v75
	v_lshl_add_u64 v[70:71], s[8:9], 0, v[70:71]
	v_addc_co_u32_e32 v81, vcc, 0, v79, vcc
	v_pk_fma_f32 v[68:69], v[68:69], v[72:73], v[74:75]
	v_lshl_add_u64 v[70:71], v[70:71], 0, v[142:143]
	v_cvt_pk_bf16_f32 v66, v66, v67
	v_cvt_pk_bf16_f32 v67, v68, v69
	v_mov_b32_e32 v68, v184
	v_mov_b32_e32 v69, v185
	v_mov_b32_e32 v72, v186
	v_mov_b32_e32 v73, v187
	v_lshl_add_u64 v[74:75], v[78:79], 0, s[10:11]
	global_store_dwordx2 v[86:87], v[66:67], off offset:288
	s_nop 0
	v_lshlrev_b32_e32 v66, 16, v68
	v_and_b32_e32 v67, 0xffff0000, v68
	v_lshlrev_b32_e32 v68, 16, v69
	v_and_b32_e32 v69, 0xffff0000, v69
	v_lshlrev_b32_e32 v76, 16, v72
	v_and_b32_e32 v77, 0xffff0000, v72
	v_lshlrev_b32_e32 v72, 16, v73
	v_and_b32_e32 v73, 0xffff0000, v73
	v_pk_fma_f32 v[64:65], v[64:65], v[68:69], v[72:73]
	v_pk_fma_f32 v[62:63], v[62:63], v[66:67], v[76:77]
	s_nop 0
	v_cvt_pk_bf16_f32 v62, v62, v63
	v_cvt_pk_bf16_f32 v63, v64, v65
	v_mov_b32_e32 v64, v188
	v_mov_b32_e32 v65, v189
	v_mov_b32_e32 v66, v190
	v_mov_b32_e32 v67, v191
	s_nop 0
	v_lshlrev_b32_e32 v68, 16, v66
	global_store_dwordx2 v[70:71], v[62:63], off
	v_lshlrev_b32_e32 v62, 16, v64
	v_and_b32_e32 v63, 0xffff0000, v64
	v_lshlrev_b32_e32 v64, 16, v65
	v_and_b32_e32 v65, 0xffff0000, v65
	v_and_b32_e32 v69, 0xffff0000, v66
	v_lshlrev_b32_e32 v66, 16, v67
	v_and_b32_e32 v67, 0xffff0000, v67
	v_pk_fma_f32 v[60:61], v[60:61], v[64:65], v[66:67]
	v_pk_fma_f32 v[58:59], v[58:59], v[62:63], v[68:69]
	s_nop 0
	v_cvt_pk_bf16_f32 v58, v58, v59
	v_cvt_pk_bf16_f32 v59, v60, v61
	v_mov_b32_e32 v60, v192
	v_mov_b32_e32 v61, v193
	v_mov_b32_e32 v62, v194
	v_mov_b32_e32 v63, v195
	s_nop 0
	v_lshlrev_b32_e32 v64, 16, v62
	global_store_dwordx2 v[70:71], v[58:59], off offset:32
	v_lshlrev_b32_e32 v58, 16, v60
	v_and_b32_e32 v59, 0xffff0000, v60
	v_lshlrev_b32_e32 v60, 16, v61
	v_and_b32_e32 v61, 0xffff0000, v61
	v_and_b32_e32 v65, 0xffff0000, v62
	v_lshlrev_b32_e32 v62, 16, v63
	v_and_b32_e32 v63, 0xffff0000, v63
	v_pk_fma_f32 v[56:57], v[56:57], v[60:61], v[62:63]
	v_pk_fma_f32 v[54:55], v[54:55], v[58:59], v[64:65]
	v_add_u32_e32 v60, 0x90, v144
	v_cvt_pk_bf16_f32 v54, v54, v55
	v_cvt_pk_bf16_f32 v55, v56, v57
	v_mov_b32_e32 v56, v196
	v_mov_b32_e32 v57, v197
	v_mov_b32_e32 v58, v198
	v_mov_b32_e32 v59, v199
	v_ashrrev_i32_e32 v61, 31, v60
	v_mad_i64_i32 v[62:63], s[22:23], v60, s47, v[146:147]
	global_store_dwordx2 v[70:71], v[54:55], off offset:256
	v_lshl_add_u64 v[62:63], v[62:63], 0, v[142:143]
	v_add_co_u32_e32 v64, vcc, s48, v62
	s_nop 0
	v_lshlrev_b32_e32 v54, 16, v56
	v_and_b32_e32 v55, 0xffff0000, v56
	v_lshlrev_b32_e32 v66, 16, v58
	v_and_b32_e32 v67, 0xffff0000, v58
	v_pk_fma_f32 v[50:51], v[50:51], v[54:55], v[66:67]
	v_lshlrev_b64 v[54:55], 12, v[60:61]
	v_lshlrev_b32_e32 v56, 16, v57
	v_and_b32_e32 v57, 0xffff0000, v57
	v_lshlrev_b32_e32 v58, 16, v59
	v_and_b32_e32 v59, 0xffff0000, v59
	v_lshl_add_u64 v[54:55], s[8:9], 0, v[54:55]
	v_addc_co_u32_e32 v65, vcc, 0, v63, vcc
	v_pk_fma_f32 v[52:53], v[52:53], v[56:57], v[58:59]
	v_lshl_add_u64 v[54:55], v[54:55], 0, v[142:143]
	v_cvt_pk_bf16_f32 v50, v50, v51
	v_cvt_pk_bf16_f32 v51, v52, v53
	v_mov_b32_e32 v52, v200
	v_mov_b32_e32 v53, v201
	v_mov_b32_e32 v56, v202
	v_mov_b32_e32 v57, v203
	v_lshl_add_u64 v[58:59], v[62:63], 0, s[10:11]
	global_store_dwordx2 v[70:71], v[50:51], off offset:288
	s_nop 0
	v_lshlrev_b32_e32 v50, 16, v52
	v_and_b32_e32 v51, 0xffff0000, v52
	v_lshlrev_b32_e32 v52, 16, v53
	v_and_b32_e32 v53, 0xffff0000, v53
	v_lshlrev_b32_e32 v60, 16, v56
	v_and_b32_e32 v61, 0xffff0000, v56
	v_lshlrev_b32_e32 v56, 16, v57
	v_and_b32_e32 v57, 0xffff0000, v57
	v_pk_fma_f32 v[48:49], v[48:49], v[52:53], v[56:57]
	v_pk_fma_f32 v[46:47], v[46:47], v[50:51], v[60:61]
	s_nop 0
	v_cvt_pk_bf16_f32 v46, v46, v47
	v_cvt_pk_bf16_f32 v47, v48, v49
	v_mov_b32_e32 v48, v204
	v_mov_b32_e32 v49, v205
	v_mov_b32_e32 v50, v206
	v_mov_b32_e32 v51, v207
	s_nop 0
	v_lshlrev_b32_e32 v52, 16, v50
	global_store_dwordx2 v[54:55], v[46:47], off
	v_lshlrev_b32_e32 v46, 16, v48
	v_and_b32_e32 v47, 0xffff0000, v48
	v_lshlrev_b32_e32 v48, 16, v49
	v_and_b32_e32 v49, 0xffff0000, v49
	v_and_b32_e32 v53, 0xffff0000, v50
	v_lshlrev_b32_e32 v50, 16, v51
	v_and_b32_e32 v51, 0xffff0000, v51
	v_pk_fma_f32 v[44:45], v[44:45], v[48:49], v[50:51]
	v_pk_fma_f32 v[42:43], v[42:43], v[46:47], v[52:53]
	s_nop 0
	v_cvt_pk_bf16_f32 v42, v42, v43
	v_cvt_pk_bf16_f32 v43, v44, v45
	v_mov_b32_e32 v44, v208
	v_mov_b32_e32 v45, v209
	v_mov_b32_e32 v46, v210
	v_mov_b32_e32 v47, v211
	s_nop 0
	v_lshlrev_b32_e32 v48, 16, v46
	global_store_dwordx2 v[54:55], v[42:43], off offset:32
	v_lshlrev_b32_e32 v42, 16, v44
	v_and_b32_e32 v43, 0xffff0000, v44
	v_lshlrev_b32_e32 v44, 16, v45
	v_and_b32_e32 v45, 0xffff0000, v45
	v_and_b32_e32 v49, 0xffff0000, v46
	v_lshlrev_b32_e32 v46, 16, v47
	v_and_b32_e32 v47, 0xffff0000, v47
	v_pk_fma_f32 v[40:41], v[40:41], v[44:45], v[46:47]
	v_pk_fma_f32 v[38:39], v[38:39], v[42:43], v[48:49]
	v_add_u32_e32 v44, 0xa0, v144
	v_cvt_pk_bf16_f32 v38, v38, v39
	v_cvt_pk_bf16_f32 v39, v40, v41
	v_mov_b32_e32 v40, v212
	v_mov_b32_e32 v41, v213
	v_mov_b32_e32 v42, v214
	v_mov_b32_e32 v43, v215
	v_ashrrev_i32_e32 v45, 31, v44
	v_mad_i64_i32 v[46:47], s[22:23], v44, s47, v[146:147]
	global_store_dwordx2 v[54:55], v[38:39], off offset:256
	v_lshl_add_u64 v[46:47], v[46:47], 0, v[142:143]
	v_add_co_u32_e32 v48, vcc, s48, v46
	s_nop 0
	v_lshlrev_b32_e32 v38, 16, v40
	v_and_b32_e32 v39, 0xffff0000, v40
	v_lshlrev_b32_e32 v50, 16, v42
	v_and_b32_e32 v51, 0xffff0000, v42
	v_pk_fma_f32 v[34:35], v[34:35], v[38:39], v[50:51]
	v_lshlrev_b64 v[38:39], 12, v[44:45]
	v_lshlrev_b32_e32 v40, 16, v41
	v_and_b32_e32 v41, 0xffff0000, v41
	v_lshlrev_b32_e32 v42, 16, v43
	v_and_b32_e32 v43, 0xffff0000, v43
	v_lshl_add_u64 v[38:39], s[8:9], 0, v[38:39]
	v_addc_co_u32_e32 v49, vcc, 0, v47, vcc
	v_pk_fma_f32 v[36:37], v[36:37], v[40:41], v[42:43]
	v_lshl_add_u64 v[38:39], v[38:39], 0, v[142:143]
	v_cvt_pk_bf16_f32 v34, v34, v35
	v_cvt_pk_bf16_f32 v35, v36, v37
	v_mov_b32_e32 v237, 0x1000
	v_mov_b32_e32 v236, 160
	v_mad_i64_i32 v[230:231], s[22:23], v236, s47, v[228:229]
	v_mad_i64_i32 v[234:235], s[22:23], v236, v237, v[232:233]
	global_load_dwordx2 v[168:169], v[230:231], off
	global_load_dwordx2 v[170:171], v[234:235], off
	global_load_dwordx2 v[172:173], v[230:231], off offset:32
	global_load_dwordx2 v[174:175], v[234:235], off offset:32
	global_load_dwordx2 v[176:177], v[230:231], off offset:256
	global_load_dwordx2 v[178:179], v[234:235], off offset:256
	global_load_dwordx2 v[180:181], v[230:231], off offset:288
	global_load_dwordx2 v[182:183], v[234:235], off offset:288
	v_mov_b32_e32 v236, 176
	v_mad_i64_i32 v[230:231], s[22:23], v236, s47, v[228:229]
	v_mad_i64_i32 v[234:235], s[22:23], v236, v237, v[232:233]
	global_load_dwordx2 v[184:185], v[230:231], off
	global_load_dwordx2 v[186:187], v[234:235], off
	global_load_dwordx2 v[188:189], v[230:231], off offset:32
	global_load_dwordx2 v[190:191], v[234:235], off offset:32
	global_load_dwordx2 v[192:193], v[230:231], off offset:256
	global_load_dwordx2 v[194:195], v[234:235], off offset:256
	global_load_dwordx2 v[196:197], v[230:231], off offset:288
	global_load_dwordx2 v[198:199], v[234:235], off offset:288
	s_waitcnt vmcnt(0)
	v_mov_b32_e32 v36, v168
	v_mov_b32_e32 v37, v169
	v_mov_b32_e32 v40, v170
	v_mov_b32_e32 v41, v171
	v_lshl_add_u64 v[42:43], v[46:47], 0, s[10:11]
	global_store_dwordx2 v[54:55], v[34:35], off offset:288
	s_nop 0
	v_lshlrev_b32_e32 v34, 16, v36
	v_and_b32_e32 v35, 0xffff0000, v36
	v_lshlrev_b32_e32 v36, 16, v37
	v_and_b32_e32 v37, 0xffff0000, v37
	v_lshlrev_b32_e32 v44, 16, v40
	v_and_b32_e32 v45, 0xffff0000, v40
	v_lshlrev_b32_e32 v40, 16, v41
	v_and_b32_e32 v41, 0xffff0000, v41
	v_pk_fma_f32 v[32:33], v[32:33], v[36:37], v[40:41]
	v_pk_fma_f32 v[30:31], v[30:31], v[34:35], v[44:45]
	s_nop 0
	v_cvt_pk_bf16_f32 v30, v30, v31
	v_cvt_pk_bf16_f32 v31, v32, v33
	v_mov_b32_e32 v32, v172
	v_mov_b32_e32 v33, v173
	v_mov_b32_e32 v34, v174
	v_mov_b32_e32 v35, v175
	s_nop 0
	v_lshlrev_b32_e32 v36, 16, v34
	global_store_dwordx2 v[38:39], v[30:31], off
	v_lshlrev_b32_e32 v30, 16, v32
	v_and_b32_e32 v31, 0xffff0000, v32
	v_lshlrev_b32_e32 v32, 16, v33
	v_and_b32_e32 v33, 0xffff0000, v33
	v_and_b32_e32 v37, 0xffff0000, v34
	v_lshlrev_b32_e32 v34, 16, v35
	v_and_b32_e32 v35, 0xffff0000, v35
	v_pk_fma_f32 v[28:29], v[28:29], v[32:33], v[34:35]
	v_pk_fma_f32 v[26:27], v[26:27], v[30:31], v[36:37]
	s_nop 0
	v_cvt_pk_bf16_f32 v26, v26, v27
	v_cvt_pk_bf16_f32 v27, v28, v29
	v_mov_b32_e32 v28, v176
	v_mov_b32_e32 v29, v177
	v_mov_b32_e32 v30, v178
	v_mov_b32_e32 v31, v179
	s_nop 0
	v_lshlrev_b32_e32 v32, 16, v30
	global_store_dwordx2 v[38:39], v[26:27], off offset:32
	v_lshlrev_b32_e32 v26, 16, v28
	v_and_b32_e32 v27, 0xffff0000, v28
	v_lshlrev_b32_e32 v28, 16, v29
	v_and_b32_e32 v29, 0xffff0000, v29
	v_and_b32_e32 v33, 0xffff0000, v30
	v_lshlrev_b32_e32 v30, 16, v31
	v_and_b32_e32 v31, 0xffff0000, v31
	v_pk_fma_f32 v[24:25], v[24:25], v[28:29], v[30:31]
	v_pk_fma_f32 v[22:23], v[22:23], v[26:27], v[32:33]
	v_add_u32_e32 v28, 0xb0, v144
	v_cvt_pk_bf16_f32 v22, v22, v23
	v_cvt_pk_bf16_f32 v23, v24, v25
	v_mov_b32_e32 v24, v180
	v_mov_b32_e32 v25, v181
	v_mov_b32_e32 v26, v182
	v_mov_b32_e32 v27, v183
	v_ashrrev_i32_e32 v29, 31, v28
	v_mad_i64_i32 v[30:31], s[22:23], v28, s47, v[146:147]
	global_store_dwordx2 v[38:39], v[22:23], off offset:256
	v_lshl_add_u64 v[30:31], v[30:31], 0, v[142:143]
	v_add_co_u32_e32 v32, vcc, s48, v30
	s_mov_b64 s[22:23], s[16:17]
	s_nop 0
	v_addc_co_u32_e32 v33, vcc, 0, v31, vcc
	s_and_b64 vcc, exec, s[0:1]
	s_nop 0
	v_lshlrev_b32_e32 v22, 16, v24
	v_and_b32_e32 v23, 0xffff0000, v24
	v_lshlrev_b32_e32 v34, 16, v26
	v_and_b32_e32 v35, 0xffff0000, v26
	v_pk_fma_f32 v[18:19], v[18:19], v[22:23], v[34:35]
	v_lshlrev_b64 v[22:23], 12, v[28:29]
	v_lshlrev_b32_e32 v24, 16, v25
	v_and_b32_e32 v25, 0xffff0000, v25
	v_lshlrev_b32_e32 v26, 16, v27
	v_and_b32_e32 v27, 0xffff0000, v27
	v_lshl_add_u64 v[22:23], s[8:9], 0, v[22:23]
	v_pk_fma_f32 v[20:21], v[20:21], v[24:25], v[26:27]
	v_lshl_add_u64 v[22:23], v[22:23], 0, v[142:143]
	v_cvt_pk_bf16_f32 v18, v18, v19
	v_cvt_pk_bf16_f32 v19, v20, v21
	v_mov_b32_e32 v20, v184
	v_mov_b32_e32 v21, v185
	v_mov_b32_e32 v24, v186
	v_mov_b32_e32 v25, v187
	v_lshl_add_u64 v[26:27], v[30:31], 0, s[10:11]
	global_store_dwordx2 v[38:39], v[18:19], off offset:288
	s_nop 0
	v_lshlrev_b32_e32 v18, 16, v20
	v_and_b32_e32 v19, 0xffff0000, v20
	v_lshlrev_b32_e32 v20, 16, v21
	v_and_b32_e32 v21, 0xffff0000, v21
	v_lshlrev_b32_e32 v28, 16, v24
	v_and_b32_e32 v29, 0xffff0000, v24
	v_lshlrev_b32_e32 v24, 16, v25
	v_and_b32_e32 v25, 0xffff0000, v25
	v_pk_fma_f32 v[16:17], v[16:17], v[20:21], v[24:25]
	v_pk_fma_f32 v[14:15], v[14:15], v[18:19], v[28:29]
	s_nop 0
	v_cvt_pk_bf16_f32 v14, v14, v15
	v_cvt_pk_bf16_f32 v15, v16, v17
	v_mov_b32_e32 v16, v188
	v_mov_b32_e32 v17, v189
	v_mov_b32_e32 v18, v190
	v_mov_b32_e32 v19, v191
	s_nop 0
	v_lshlrev_b32_e32 v20, 16, v18
	global_store_dwordx2 v[22:23], v[14:15], off
	v_lshlrev_b32_e32 v14, 16, v16
	v_and_b32_e32 v15, 0xffff0000, v16
	v_lshlrev_b32_e32 v16, 16, v17
	v_and_b32_e32 v17, 0xffff0000, v17
	v_and_b32_e32 v21, 0xffff0000, v18
	v_lshlrev_b32_e32 v18, 16, v19
	v_and_b32_e32 v19, 0xffff0000, v19
	v_pk_fma_f32 v[12:13], v[12:13], v[16:17], v[18:19]
	v_pk_fma_f32 v[10:11], v[10:11], v[14:15], v[20:21]
	s_nop 0
	v_cvt_pk_bf16_f32 v10, v10, v11
	v_cvt_pk_bf16_f32 v11, v12, v13
	v_mov_b32_e32 v12, v192
	v_mov_b32_e32 v13, v193
	v_mov_b32_e32 v14, v194
	v_mov_b32_e32 v15, v195
	s_nop 0
	v_lshlrev_b32_e32 v16, 16, v14
	global_store_dwordx2 v[22:23], v[10:11], off offset:32
	v_lshlrev_b32_e32 v10, 16, v12
	v_and_b32_e32 v11, 0xffff0000, v12
	v_lshlrev_b32_e32 v12, 16, v13
	v_and_b32_e32 v13, 0xffff0000, v13
	v_and_b32_e32 v17, 0xffff0000, v14
	v_lshlrev_b32_e32 v14, 16, v15
	v_and_b32_e32 v15, 0xffff0000, v15
	v_pk_fma_f32 v[8:9], v[8:9], v[12:13], v[14:15]
	v_pk_fma_f32 v[6:7], v[6:7], v[10:11], v[16:17]
	s_nop 0
	v_cvt_pk_bf16_f32 v6, v6, v7
	v_cvt_pk_bf16_f32 v7, v8, v9
	v_mov_b32_e32 v8, v196
	v_mov_b32_e32 v9, v197
	v_mov_b32_e32 v10, v198
	v_mov_b32_e32 v11, v199
	s_nop 0
	v_lshlrev_b32_e32 v12, 16, v10
	global_store_dwordx2 v[22:23], v[6:7], off offset:256
	v_lshlrev_b32_e32 v6, 16, v8
	v_and_b32_e32 v7, 0xffff0000, v8
	v_and_b32_e32 v13, 0xffff0000, v10
	v_lshlrev_b32_e32 v8, 16, v9
	v_and_b32_e32 v9, 0xffff0000, v9
	v_lshlrev_b32_e32 v10, 16, v11
	v_and_b32_e32 v11, 0xffff0000, v11
	v_pk_fma_f32 v[2:3], v[2:3], v[6:7], v[12:13]
	v_pk_fma_f32 v[4:5], v[4:5], v[8:9], v[10:11]
	v_cvt_pk_bf16_f32 v2, v2, v3
	s_nop 0
	v_cvt_pk_bf16_f32 v3, v4, v5
	global_store_dwordx2 v[22:23], v[2:3], off offset:288
	s_cbranch_vccz .LBB0_3252
	s_waitcnt vmcnt(0)
	s_cmpk_gt_u32 s28, 0xff
	s_cbranch_scc1 .LBB0_3259
	s_barrier
